# removed the 1-wait-state s_nop 0 pads that hipcc placed after packed-f32 (VOP3P, full-dword result) producers in the FFT passes; ISA lists no hazard for full-dword results
# baseline (speedup 1.0000x reference)
.LBB0_634:
	s_or_b64 exec, exec, s[0:1]
	v_readlane_b32 s0, v251, 28
	v_mov_b32_e32 v90, v173
	v_mov_b32_e32 v2, s0
	v_readlane_b32 s0, v251, 34
	v_mov_b32_e32 v10, v1
	s_waitcnt lgkmcnt(0)
	v_mov_b32_e32 v3, s0
	s_barrier
	ds_read_b128 v[6:9], v2
	ds_read_b128 v[2:5], v3
	v_mov_b32_e32 v60, v164
	v_mov_b32_e32 v34, v165
	v_mov_b32_e32 v62, v166
	v_mov_b32_e32 v32, v167
	v_mov_b32_e32 v64, v168
	v_mov_b32_e32 v38, v169
	v_mov_b32_e32 v66, v170
	v_mov_b32_e32 v10, v171
	v_pk_add_f32 v[68:69], v[14:15], v[42:43]
	v_pk_add_f32 v[14:15], v[14:15], v[42:43] neg_lo:[0,1] neg_hi:[0,1]
	v_mov_b32_e32 v13, v15
	v_mov_b32_e32 v10, v14
	v_mov_b32_e32 v42, v15
	v_mov_b32_e32 v43, v11
	v_pk_mul_f32 v[14:15], v[12:13], v[66:67] op_sel_hi:[1,0] neg_lo:[0,1] neg_hi:[0,1]
	v_pk_add_f32 v[70:71], v[18:19], v[52:53]
	v_pk_fma_f32 v[42:43], v[42:43], v[60:61], v[14:15] op_sel_hi:[1,0,1]
	v_pk_add_f32 v[14:15], v[16:17], v[48:49]
	v_pk_add_f32 v[48:49], v[16:17], v[48:49] neg_lo:[0,1] neg_hi:[0,1]
	v_mov_b32_e32 v17, v11
	v_mov_b32_e32 v13, v48
	v_mov_b32_e32 v16, v48
	v_pk_mul_f32 v[54:55], v[12:13], v[38:39] op_sel_hi:[1,0] neg_lo:[0,1] neg_hi:[0,1]
	v_mov_b32_e32 v13, v49
	v_pk_add_f32 v[18:19], v[18:19], v[52:53] neg_lo:[0,1] neg_hi:[0,1]
	v_pk_fma_f32 v[16:17], v[16:17], v[34:35], v[54:55] op_sel_hi:[1,0,1]
	v_mov_b32_e32 v54, v49
	v_mov_b32_e32 v55, v11
	v_pk_mul_f32 v[48:49], v[12:13], v[64:65] op_sel_hi:[1,0] neg_lo:[0,1] neg_hi:[0,1]
	v_mov_b32_e32 v13, v18
	v_pk_fma_f32 v[48:49], v[54:55], v[62:63], v[48:49] op_sel_hi:[1,0,1]
	v_mov_b32_e32 v52, v18
	v_mov_b32_e32 v53, v11
	v_pk_mul_f32 v[54:55], v[12:13], v[32:33] op_sel_hi:[1,0] neg_lo:[0,1] neg_hi:[0,1]
	v_mov_b32_e32 v13, v19
	v_pk_fma_f32 v[52:53], v[52:53], v[32:33], v[54:55] op_sel_hi:[1,0,1]
	v_mov_b32_e32 v54, v19
	v_mov_b32_e32 v55, v11
	v_pk_add_f32 v[18:19], v[20:21], v[50:51]
	v_pk_add_f32 v[20:21], v[20:21], v[50:51] neg_lo:[0,1] neg_hi:[0,1]
	v_pk_mul_f32 v[54:55], v[54:55], v[64:65] op_sel_hi:[1,0]
	v_mov_b32_e32 v50, v20
	v_mov_b32_e32 v51, v11
	v_pk_fma_f32 v[54:55], v[12:13], v[62:63], v[54:55] op_sel_hi:[1,0,1] neg_lo:[0,1,0] neg_hi:[0,1,0]
	v_pk_mul_f32 v[50:51], v[50:51], v[38:39] op_sel_hi:[1,0]
	v_mov_b32_e32 v13, v20
	v_pk_fma_f32 v[58:59], v[12:13], v[34:35], v[50:51] op_sel_hi:[1,0,1] neg_lo:[0,1,0] neg_hi:[0,1,0]
	v_mov_b32_e32 v50, v21
	v_mov_b32_e32 v51, v11
	v_pk_mul_f32 v[50:51], v[50:51], v[66:67] op_sel_hi:[1,0]
	v_mov_b32_e32 v13, v21
	v_pk_add_f32 v[20:21], v[26:27], v[46:47]
	v_pk_add_f32 v[26:27], v[26:27], v[46:47] neg_lo:[0,1] neg_hi:[0,1]
	v_pk_fma_f32 v[56:57], v[12:13], v[60:61], v[50:51] op_sel_hi:[1,0,1] neg_lo:[0,1,0] neg_hi:[0,1,0]
	v_xor_b32_e32 v73, 0x80000000, v26
	v_mov_b32_e32 v46, v27
	v_mov_b32_e32 v47, v11
	v_mov_b32_e32 v13, v27
	v_pk_add_f32 v[26:27], v[30:31], v[44:45]
	v_pk_add_f32 v[30:31], v[30:31], v[44:45] neg_lo:[0,1] neg_hi:[0,1]
	v_pk_mul_f32 v[46:47], v[46:47], v[66:67] op_sel_hi:[1,0] neg_lo:[0,1] neg_hi:[0,1]
	v_mov_b32_e32 v44, v30
	v_mov_b32_e32 v45, v11
	v_pk_fma_f32 v[74:75], v[12:13], v[60:61], v[46:47] op_sel_hi:[1,0,1] neg_lo:[0,1,0] neg_hi:[0,1,0]
	v_pk_mul_f32 v[44:45], v[44:45], v[38:39] op_sel_hi:[1,0] neg_lo:[0,1] neg_hi:[0,1]
	v_mov_b32_e32 v13, v30
	v_pk_fma_f32 v[76:77], v[12:13], v[34:35], v[44:45] op_sel_hi:[1,0,1] neg_lo:[0,1,0] neg_hi:[0,1,0]
	v_mov_b32_e32 v44, v31
	v_mov_b32_e32 v45, v11
	v_pk_mul_f32 v[44:45], v[44:45], v[64:65] op_sel_hi:[1,0] neg_lo:[0,1] neg_hi:[0,1]
	v_mov_b32_e32 v13, v31
	v_pk_add_f32 v[30:31], v[28:29], v[40:41]
	v_pk_add_f32 v[28:29], v[28:29], v[40:41] neg_lo:[0,1] neg_hi:[0,1]
	v_pk_fma_f32 v[78:79], v[12:13], v[62:63], v[44:45] op_sel_hi:[1,0,1] neg_lo:[0,1,0] neg_hi:[0,1,0]
	v_mov_b32_e32 v13, v28
	v_mov_b32_e32 v40, v28
	v_mov_b32_e32 v41, v11
	v_pk_mul_f32 v[44:45], v[12:13], v[32:33] op_sel_hi:[1,0] neg_lo:[0,1] neg_hi:[0,1]
	v_mov_b32_e32 v13, v29
	v_pk_fma_f32 v[80:81], v[40:41], v[32:33], v[44:45] op_sel_hi:[1,0,1] neg_lo:[0,1,0] neg_hi:[0,1,0]
	v_mov_b32_e32 v40, v29
	v_pk_mul_f32 v[28:29], v[12:13], v[64:65] op_sel_hi:[1,0] neg_lo:[0,1] neg_hi:[0,1]
	v_mov_b32_e32 v45, v11
	v_pk_fma_f32 v[62:63], v[40:41], v[62:63], v[28:29] op_sel_hi:[1,0,1] neg_lo:[0,1,0] neg_hi:[0,1,0]
	v_pk_add_f32 v[28:29], v[24:25], v[36:37]
	v_pk_add_f32 v[24:25], v[24:25], v[36:37] neg_lo:[0,1] neg_hi:[0,1]
	v_mov_b32_e32 v37, v11
	v_mov_b32_e32 v13, v24
	v_mov_b32_e32 v36, v24
	v_pk_mul_f32 v[40:41], v[12:13], v[38:39] op_sel_hi:[1,0] neg_lo:[0,1] neg_hi:[0,1]
	v_mov_b32_e32 v13, v25
	v_pk_fma_f32 v[64:65], v[36:37], v[34:35], v[40:41] op_sel_hi:[1,0,1] neg_lo:[0,1,0] neg_hi:[0,1,0]
	v_mov_b32_e32 v36, v25
	v_pk_mul_f32 v[24:25], v[12:13], v[66:67] op_sel_hi:[1,0] neg_lo:[0,1] neg_hi:[0,1]
	v_mov_b32_e32 v41, v11
	v_pk_fma_f32 v[66:67], v[36:37], v[60:61], v[24:25] op_sel_hi:[1,0,1] neg_lo:[0,1,0] neg_hi:[0,1,0]
	v_pk_add_f32 v[24:25], v[68:69], v[20:21] neg_lo:[0,1] neg_hi:[0,1]
	v_pk_add_f32 v[20:21], v[68:69], v[20:21]
	v_mov_b32_e32 v13, v25
	v_mov_b32_e32 v36, v24
	v_mov_b32_e32 v40, v25
	v_pk_mul_f32 v[24:25], v[12:13], v[38:39] op_sel_hi:[1,0] neg_lo:[0,1] neg_hi:[0,1]
	v_mov_b32_e32 v69, v11
	v_pk_fma_f32 v[24:25], v[40:41], v[34:35], v[24:25] op_sel_hi:[1,0,1]
	v_pk_add_f32 v[40:41], v[14:15], v[26:27] neg_lo:[0,1] neg_hi:[0,1]
	v_pk_add_f32 v[14:15], v[14:15], v[26:27]
	v_mov_b32_e32 v13, v40
	v_mov_b32_e32 v44, v40
	v_pk_mul_f32 v[46:47], v[12:13], v[32:33] op_sel_hi:[1,0] neg_lo:[0,1] neg_hi:[0,1]
	v_mov_b32_e32 v13, v41
	v_pk_fma_f32 v[44:45], v[44:45], v[32:33], v[46:47] op_sel_hi:[1,0,1]
	v_mov_b32_e32 v46, v41
	v_mov_b32_e32 v47, v11
	v_pk_mul_f32 v[46:47], v[46:47], v[38:39] op_sel_hi:[1,0]
	v_pk_add_f32 v[40:41], v[70:71], v[30:31] neg_lo:[0,1] neg_hi:[0,1]
	v_pk_fma_f32 v[50:51], v[12:13], v[34:35], v[46:47] op_sel_hi:[1,0,1] neg_lo:[0,1,0] neg_hi:[0,1,0]
	v_mov_b32_e32 v46, v41
	v_mov_b32_e32 v47, v11
	v_xor_b32_e32 v83, 0x80000000, v40
	v_pk_mul_f32 v[46:47], v[46:47], v[38:39] op_sel_hi:[1,0] neg_lo:[0,1] neg_hi:[0,1]
	v_mov_b32_e32 v13, v41
	v_pk_add_f32 v[40:41], v[18:19], v[28:29] neg_lo:[0,1] neg_hi:[0,1]
	v_pk_fma_f32 v[84:85], v[12:13], v[34:35], v[46:47] op_sel_hi:[1,0,1] neg_lo:[0,1,0] neg_hi:[0,1,0]
	v_mov_b32_e32 v13, v40
	v_pk_add_f32 v[26:27], v[70:71], v[30:31]
	v_mov_b32_e32 v46, v40
	v_mov_b32_e32 v47, v11
	v_pk_mul_f32 v[60:61], v[12:13], v[32:33] op_sel_hi:[1,0] neg_lo:[0,1] neg_hi:[0,1]
	v_mov_b32_e32 v13, v41
	v_pk_add_f32 v[18:19], v[18:19], v[28:29]
	v_pk_add_f32 v[28:29], v[20:21], v[26:27] neg_lo:[0,1] neg_hi:[0,1]
	v_pk_fma_f32 v[86:87], v[46:47], v[32:33], v[60:61] op_sel_hi:[1,0,1] neg_lo:[0,1,0] neg_hi:[0,1,0]
	v_mov_b32_e32 v46, v41
	v_pk_mul_f32 v[40:41], v[12:13], v[38:39] op_sel_hi:[1,0] neg_lo:[0,1] neg_hi:[0,1]
	v_mov_b32_e32 v13, v29
	v_pk_fma_f32 v[88:89], v[46:47], v[34:35], v[40:41] op_sel_hi:[1,0,1] neg_lo:[0,1,0] neg_hi:[0,1,0]
	v_mov_b32_e32 v40, v28
	v_pk_add_f32 v[20:21], v[20:21], v[26:27]
	v_mov_b32_e32 v26, v29
	v_mov_b32_e32 v27, v11
	v_pk_mul_f32 v[28:29], v[12:13], v[32:33] op_sel_hi:[1,0] neg_lo:[0,1] neg_hi:[0,1]
	v_mov_b32_e32 v41, v11
	v_pk_fma_f32 v[26:27], v[26:27], v[32:33], v[28:29] op_sel_hi:[1,0,1]
	v_pk_add_f32 v[28:29], v[14:15], v[18:19] neg_lo:[0,1] neg_hi:[0,1]
	v_pk_add_f32 v[14:15], v[14:15], v[18:19]
	v_mov_b32_e32 v13, v29
	v_xor_b32_e32 v61, 0x80000000, v28
	v_mov_b32_e32 v18, v29
	v_mov_b32_e32 v19, v11
	v_pk_mul_f32 v[28:29], v[12:13], v[32:33] op_sel_hi:[1,0] neg_lo:[0,1] neg_hi:[0,1]
	v_pk_add_f32 v[30:31], v[20:21], v[14:15]
	v_pk_fma_f32 v[18:19], v[18:19], v[32:33], v[28:29] op_sel_hi:[1,0,1] neg_lo:[0,1,0] neg_hi:[0,1,0]
	v_pk_add_f32 v[28:29], v[20:21], v[14:15] neg_lo:[0,1] neg_hi:[0,1]
	v_mov_b32_e32 v60, v11
	v_pk_add_f32 v[14:15], v[28:29], 0 neg_lo:[1,1] neg_hi:[1,1]
	v_mov_b32_e32 v68, v28
	v_mov_b32_e32 v14, v11
	v_pk_add_f32 v[46:47], v[68:69], v[14:15]
	v_pk_add_f32 v[20:21], v[68:69], v[14:15] neg_lo:[0,1] neg_hi:[0,1]
	v_pk_add_f32 v[14:15], v[40:41], v[60:61]
	v_pk_add_f32 v[28:29], v[40:41], v[60:61] neg_lo:[0,1] neg_hi:[0,1]
	v_pk_add_f32 v[40:41], v[26:27], v[18:19]
	v_pk_add_f32 v[18:19], v[26:27], v[18:19] neg_lo:[0,1] neg_hi:[0,1]
	v_mov_b32_e32 v82, v11
	v_pk_add_f32 v[60:61], v[14:15], v[40:41]
	v_pk_add_f32 v[26:27], v[14:15], v[40:41] neg_lo:[0,1] neg_hi:[0,1]
	v_pk_add_f32 v[40:41], v[28:29], v[18:19] op_sel:[0,1] op_sel_hi:[1,0] neg_hi:[0,1]
	v_pk_add_f32 v[14:15], v[28:29], v[18:19] op_sel:[0,1] op_sel_hi:[1,0] neg_lo:[0,1]
	v_pk_add_f32 v[18:19], v[36:37], v[82:83]
	v_pk_add_f32 v[28:29], v[36:37], v[82:83] neg_lo:[0,1] neg_hi:[0,1]
	v_pk_add_f32 v[36:37], v[24:25], v[84:85]
	v_pk_add_f32 v[24:25], v[24:25], v[84:85] neg_lo:[0,1] neg_hi:[0,1]
	v_mov_b32_e32 v72, v11
	v_pk_mul_f32 v[68:69], v[32:33], v[24:25] op_sel:[0,1] op_sel_hi:[0,0] neg_lo:[1,1] neg_hi:[1,0]
	v_pk_fma_f32 v[68:69], v[32:33], v[24:25], v[68:69] op_sel_hi:[0,1,1]
	v_pk_add_f32 v[24:25], v[44:45], v[86:87]
	v_pk_add_f32 v[44:45], v[44:45], v[86:87] neg_lo:[0,1] neg_hi:[0,1]
	v_lshl_add_u32 v13, v90, 3, 0
	v_xor_b32_e32 v71, 0x80000000, v44
	v_mov_b32_e32 v70, v45
	v_pk_add_f32 v[44:45], v[50:51], v[88:89]
	v_pk_add_f32 v[50:51], v[50:51], v[88:89] neg_lo:[0,1] neg_hi:[0,1]
	v_pk_mul_f32 v[82:83], v[32:33], v[50:51] op_sel:[0,1] op_sel_hi:[0,0] neg_lo:[1,1] neg_hi:[1,0]
	v_pk_fma_f32 v[82:83], v[32:33], v[50:51], v[82:83] op_sel_hi:[0,1,1] neg_lo:[1,0,0] neg_hi:[1,0,0]
	v_pk_add_f32 v[50:51], v[18:19], v[24:25]
	v_pk_add_f32 v[18:19], v[18:19], v[24:25] neg_lo:[0,1] neg_hi:[0,1]
	v_pk_add_f32 v[24:25], v[36:37], v[44:45]
	v_pk_add_f32 v[36:37], v[36:37], v[44:45] neg_lo:[0,1] neg_hi:[0,1]
	v_pk_add_f32 v[84:85], v[50:51], v[24:25]
	v_xor_b32_e32 v45, 0x80000000, v36
	v_mov_b32_e32 v44, v37
	v_pk_add_f32 v[36:37], v[50:51], v[24:25] neg_lo:[0,1] neg_hi:[0,1]
	v_pk_add_f32 v[50:51], v[18:19], v[44:45]
	v_pk_add_f32 v[24:25], v[18:19], v[44:45] neg_lo:[0,1] neg_hi:[0,1]
	v_pk_add_f32 v[44:45], v[68:69], v[82:83] neg_lo:[0,1] neg_hi:[0,1]
	v_pk_add_f32 v[18:19], v[28:29], v[70:71]
	v_pk_add_f32 v[70:71], v[28:29], v[70:71] neg_lo:[0,1] neg_hi:[0,1]
	v_pk_add_f32 v[28:29], v[68:69], v[82:83]
	v_xor_b32_e32 v69, 0x80000000, v44
	v_mov_b32_e32 v68, v45
	v_pk_add_f32 v[82:83], v[18:19], v[28:29]
	v_pk_add_f32 v[28:29], v[18:19], v[28:29] neg_lo:[0,1] neg_hi:[0,1]
	v_pk_add_f32 v[44:45], v[70:71], v[68:69]
	v_pk_add_f32 v[18:19], v[70:71], v[68:69] neg_lo:[0,1] neg_hi:[0,1]
	v_pk_add_f32 v[68:69], v[10:11], v[72:73]
	v_pk_add_f32 v[70:71], v[10:11], v[72:73] neg_lo:[0,1] neg_hi:[0,1]
	v_pk_add_f32 v[72:73], v[42:43], v[74:75]
	v_pk_add_f32 v[42:43], v[42:43], v[74:75] neg_lo:[0,1] neg_hi:[0,1]
	v_add_f32_e32 v10, v30, v31
	v_pk_mul_f32 v[74:75], v[38:39], v[42:43] op_sel:[0,1] op_sel_hi:[0,0] neg_lo:[1,1] neg_hi:[1,0]
	v_pk_fma_f32 v[42:43], v[34:35], v[42:43], v[74:75] op_sel_hi:[0,1,1]
	v_pk_add_f32 v[74:75], v[16:17], v[76:77]
	v_pk_add_f32 v[16:17], v[16:17], v[76:77] neg_lo:[0,1] neg_hi:[0,1]
	v_pk_mul_f32 v[76:77], v[32:33], v[16:17] op_sel:[0,1] op_sel_hi:[0,0] neg_lo:[1,1] neg_hi:[1,0]
	v_pk_fma_f32 v[16:17], v[32:33], v[16:17], v[76:77] op_sel_hi:[0,1,1]
	v_pk_add_f32 v[76:77], v[48:49], v[78:79]
	v_pk_add_f32 v[48:49], v[48:49], v[78:79] neg_lo:[0,1] neg_hi:[0,1]
	v_pk_mul_f32 v[78:79], v[34:35], v[48:49] op_sel:[0,1] op_sel_hi:[0,0] neg_lo:[1,1] neg_hi:[1,0]
	v_pk_fma_f32 v[78:79], v[38:39], v[48:49], v[78:79] op_sel_hi:[0,1,1]
	v_pk_add_f32 v[48:49], v[52:53], v[80:81]
	v_pk_add_f32 v[52:53], v[52:53], v[80:81] neg_lo:[0,1] neg_hi:[0,1]
	v_xor_b32_e32 v81, 0x80000000, v52
	v_mov_b32_e32 v80, v53
	v_pk_add_f32 v[52:53], v[54:55], v[62:63]
	v_pk_add_f32 v[54:55], v[54:55], v[62:63] neg_lo:[0,1] neg_hi:[0,1]
	v_pk_mul_f32 v[62:63], v[34:35], v[54:55] op_sel:[0,1] op_sel_hi:[0,0] neg_lo:[1,1] neg_hi:[1,0]
	v_pk_fma_f32 v[62:63], v[38:39], v[54:55], v[62:63] op_sel_hi:[0,1,1] neg_lo:[1,0,0] neg_hi:[1,0,0]
	v_pk_add_f32 v[54:55], v[58:59], v[64:65]
	v_pk_add_f32 v[58:59], v[58:59], v[64:65] neg_lo:[0,1] neg_hi:[0,1]
	v_pk_mul_f32 v[64:65], v[32:33], v[58:59] op_sel:[0,1] op_sel_hi:[0,0] neg_lo:[1,1] neg_hi:[1,0]
	v_pk_fma_f32 v[58:59], v[32:33], v[58:59], v[64:65] op_sel_hi:[0,1,1] neg_lo:[1,0,0] neg_hi:[1,0,0]
	v_pk_add_f32 v[64:65], v[56:57], v[66:67]
	v_pk_add_f32 v[56:57], v[56:57], v[66:67] neg_lo:[0,1] neg_hi:[0,1]
	v_pk_mul_f32 v[38:39], v[38:39], v[56:57] op_sel:[0,1] op_sel_hi:[0,0] neg_lo:[1,1] neg_hi:[1,0]
	v_pk_fma_f32 v[56:57], v[34:35], v[56:57], v[38:39] op_sel_hi:[0,1,1] neg_lo:[1,0,0] neg_hi:[1,0,0]
	v_pk_add_f32 v[38:39], v[52:53], v[72:73]
	v_pk_add_f32 v[52:53], v[72:73], v[52:53] neg_lo:[0,1] neg_hi:[0,1]
	v_pk_add_f32 v[34:35], v[68:69], v[48:49]
	v_pk_mul_f32 v[66:67], v[32:33], v[52:53] op_sel:[0,1] op_sel_hi:[0,0] neg_lo:[1,1] neg_hi:[1,0]
	v_pk_fma_f32 v[52:53], v[32:33], v[52:53], v[66:67] op_sel_hi:[0,1,1]
	v_pk_add_f32 v[66:67], v[74:75], v[54:55]
	v_pk_add_f32 v[54:55], v[74:75], v[54:55] neg_lo:[0,1] neg_hi:[0,1]
	v_pk_add_f32 v[48:49], v[68:69], v[48:49] neg_lo:[0,1] neg_hi:[0,1]
	v_xor_b32_e32 v69, 0x80000000, v54
	v_mov_b32_e32 v68, v55
	v_pk_add_f32 v[54:55], v[76:77], v[64:65]
	v_pk_add_f32 v[64:65], v[76:77], v[64:65] neg_lo:[0,1] neg_hi:[0,1]
	v_pk_mul_f32 v[72:73], v[32:33], v[64:65] op_sel:[0,1] op_sel_hi:[0,0] neg_lo:[1,1] neg_hi:[1,0]
	v_pk_fma_f32 v[64:65], v[32:33], v[64:65], v[72:73] op_sel_hi:[0,1,1] neg_lo:[1,0,0] neg_hi:[1,0,0]
	v_pk_add_f32 v[72:73], v[34:35], v[66:67]
	v_pk_add_f32 v[34:35], v[34:35], v[66:67] neg_lo:[0,1] neg_hi:[0,1]
	v_pk_add_f32 v[66:67], v[38:39], v[54:55]
	v_pk_add_f32 v[38:39], v[38:39], v[54:55] neg_lo:[0,1] neg_hi:[0,1]
	v_pk_add_f32 v[76:77], v[72:73], v[66:67]
	v_pk_add_f32 v[54:55], v[72:73], v[66:67] neg_lo:[0,1] neg_hi:[0,1]
	v_pk_add_f32 v[66:67], v[34:35], v[38:39] op_sel:[0,1] op_sel_hi:[1,0] neg_hi:[0,1]
	v_pk_add_f32 v[38:39], v[34:35], v[38:39] op_sel:[0,1] op_sel_hi:[1,0] neg_lo:[0,1]
	v_pk_add_f32 v[34:35], v[48:49], v[68:69]
	v_pk_add_f32 v[68:69], v[48:49], v[68:69] neg_lo:[0,1] neg_hi:[0,1]
	v_pk_add_f32 v[48:49], v[52:53], v[64:65]
	v_pk_add_f32 v[52:53], v[52:53], v[64:65] neg_lo:[0,1] neg_hi:[0,1]
	v_pk_add_f32 v[72:73], v[34:35], v[48:49]
	v_pk_add_f32 v[48:49], v[34:35], v[48:49] neg_lo:[0,1] neg_hi:[0,1]
	v_pk_add_f32 v[74:75], v[68:69], v[52:53] op_sel:[0,1] op_sel_hi:[1,0] neg_hi:[0,1]
	v_pk_add_f32 v[34:35], v[68:69], v[52:53] op_sel:[0,1] op_sel_hi:[1,0] neg_lo:[0,1]
	v_pk_add_f32 v[68:69], v[62:63], v[42:43]
	v_pk_add_f32 v[42:43], v[42:43], v[62:63] neg_lo:[0,1] neg_hi:[0,1]
	v_pk_add_f32 v[52:53], v[70:71], v[80:81]
	v_pk_mul_f32 v[62:63], v[32:33], v[42:43] op_sel:[0,1] op_sel_hi:[0,0] neg_lo:[1,1] neg_hi:[1,0]
	v_pk_fma_f32 v[62:63], v[32:33], v[42:43], v[62:63] op_sel_hi:[0,1,1]
	v_pk_add_f32 v[42:43], v[16:17], v[58:59]
	v_pk_add_f32 v[16:17], v[16:17], v[58:59] neg_lo:[0,1] neg_hi:[0,1]
	v_pk_add_f32 v[64:65], v[70:71], v[80:81] neg_lo:[0,1] neg_hi:[0,1]
	v_xor_b32_e32 v59, 0x80000000, v16
	v_mov_b32_e32 v58, v17
	v_pk_add_f32 v[16:17], v[78:79], v[56:57]
	v_pk_add_f32 v[56:57], v[78:79], v[56:57] neg_lo:[0,1] neg_hi:[0,1]
	v_pk_mul_f32 v[70:71], v[32:33], v[56:57] op_sel:[0,1] op_sel_hi:[0,0] neg_lo:[1,1] neg_hi:[1,0]
	v_pk_fma_f32 v[32:33], v[32:33], v[56:57], v[70:71] op_sel_hi:[0,1,1] neg_lo:[1,0,0] neg_hi:[1,0,0]
	v_pk_add_f32 v[56:57], v[52:53], v[42:43]
	v_pk_add_f32 v[42:43], v[52:53], v[42:43] neg_lo:[0,1] neg_hi:[0,1]
	v_pk_add_f32 v[52:53], v[68:69], v[16:17]
	v_pk_add_f32 v[16:17], v[68:69], v[16:17] neg_lo:[0,1] neg_hi:[0,1]
	v_pk_add_f32 v[70:71], v[56:57], v[52:53]
	v_xor_b32_e32 v69, 0x80000000, v16
	v_mov_b32_e32 v68, v17
	v_pk_add_f32 v[56:57], v[56:57], v[52:53] neg_lo:[0,1] neg_hi:[0,1]
	v_pk_add_f32 v[16:17], v[64:65], v[58:59]
	v_pk_add_f32 v[52:53], v[62:63], v[32:33]
	v_pk_add_f32 v[32:33], v[62:63], v[32:33] neg_lo:[0,1] neg_hi:[0,1]
	v_pk_add_f32 v[58:59], v[64:65], v[58:59] neg_lo:[0,1] neg_hi:[0,1]
	v_pk_add_f32 v[64:65], v[16:17], v[52:53]
	v_pk_add_f32 v[52:53], v[16:17], v[52:53] neg_lo:[0,1] neg_hi:[0,1]
	v_mov_b64_e32 v[16:17], s[90:91]
	v_pk_add_f32 v[78:79], v[42:43], v[68:69]
	v_pk_add_f32 v[42:43], v[42:43], v[68:69] neg_lo:[0,1] neg_hi:[0,1]
	v_pk_add_f32 v[68:69], v[58:59], v[32:33] op_sel:[0,1] op_sel_hi:[1,0] neg_hi:[0,1]
	v_pk_add_f32 v[32:33], v[58:59], v[32:33] op_sel:[0,1] op_sel_hi:[1,0] neg_lo:[0,1]
	v_pk_fma_f32 v[58:59], v[10:11], s[94:95], v[16:17] op_sel_hi:[0,1,1]
	ds_write_b64 v13, v[58:59]
	v_pk_fma_f32 v[58:59], v[178:179], s[90:91], v[178:179] op_sel:[1,0,0] op_sel_hi:[0,1,1]
	v_pk_mul_f32 v[62:63], v[58:59], v[76:77] op_sel:[1,1] op_sel_hi:[0,1] neg_lo:[0,1]
	v_pk_fma_f32 v[62:63], v[58:59], v[76:77], v[62:63] op_sel_hi:[1,0,1]
	ds_write_b64 v13, v[62:63] offset:4224
	v_pk_mul_f32 v[62:63], v[178:179], v[58:59] op_sel:[1,1] op_sel_hi:[0,1] neg_lo:[0,1]
	v_pk_fma_f32 v[58:59], v[178:179], v[58:59], v[62:63] op_sel_hi:[1,0,1]
	v_pk_mul_f32 v[62:63], v[58:59], v[84:85] op_sel:[1,1] op_sel_hi:[0,1] neg_lo:[0,1]
	v_pk_fma_f32 v[62:63], v[58:59], v[84:85], v[62:63] op_sel_hi:[1,0,1]
	ds_write_b64 v13, v[62:63] offset:8448
	v_pk_mul_f32 v[62:63], v[178:179], v[58:59] op_sel:[1,1] op_sel_hi:[0,1] neg_lo:[0,1]
	v_pk_fma_f32 v[58:59], v[178:179], v[58:59], v[62:63] op_sel_hi:[1,0,1]
	v_pk_mul_f32 v[62:63], v[58:59], v[70:71] op_sel:[1,1] op_sel_hi:[0,1] neg_lo:[0,1]
	v_pk_fma_f32 v[62:63], v[58:59], v[70:71], v[62:63] op_sel_hi:[1,0,1]
	ds_write_b64 v13, v[62:63] offset:12672
	v_pk_mul_f32 v[62:63], v[178:179], v[58:59] op_sel:[1,1] op_sel_hi:[0,1] neg_lo:[0,1]
	v_pk_fma_f32 v[58:59], v[178:179], v[58:59], v[62:63] op_sel_hi:[1,0,1]
	v_pk_mul_f32 v[62:63], v[60:61], v[58:59] op_sel:[1,1] op_sel_hi:[1,0] neg_lo:[1,0]
	v_pk_fma_f32 v[60:61], v[60:61], v[58:59], v[62:63] op_sel_hi:[0,1,1]
	ds_write_b64 v13, v[60:61] offset:16896
	v_pk_mul_f32 v[60:61], v[178:179], v[58:59] op_sel:[1,1] op_sel_hi:[0,1] neg_lo:[0,1]
	v_pk_fma_f32 v[58:59], v[178:179], v[58:59], v[60:61] op_sel_hi:[1,0,1]
	v_pk_mul_f32 v[60:61], v[58:59], v[72:73] op_sel:[1,1] op_sel_hi:[0,1] neg_lo:[0,1]
	v_pk_fma_f32 v[60:61], v[58:59], v[72:73], v[60:61] op_sel_hi:[1,0,1]
	ds_write_b64 v13, v[60:61] offset:21120
	v_pk_mul_f32 v[60:61], v[178:179], v[58:59] op_sel:[1,1] op_sel_hi:[0,1] neg_lo:[0,1]
	v_pk_fma_f32 v[58:59], v[178:179], v[58:59], v[60:61] op_sel_hi:[1,0,1]
	v_pk_mul_f32 v[60:61], v[82:83], v[58:59] op_sel:[1,1] op_sel_hi:[1,0] neg_lo:[1,0]
	v_pk_fma_f32 v[60:61], v[82:83], v[58:59], v[60:61] op_sel_hi:[0,1,1]
	ds_write_b64 v13, v[60:61] offset:25344
	v_pk_mul_f32 v[60:61], v[178:179], v[58:59] op_sel:[1,1] op_sel_hi:[0,1] neg_lo:[0,1]
	v_pk_fma_f32 v[58:59], v[178:179], v[58:59], v[60:61] op_sel_hi:[1,0,1]
	v_pk_mul_f32 v[60:61], v[64:65], v[58:59] op_sel:[1,1] op_sel_hi:[1,0] neg_lo:[1,0]
	v_pk_fma_f32 v[60:61], v[64:65], v[58:59], v[60:61] op_sel_hi:[0,1,1]
	ds_write_b64 v13, v[60:61] offset:29568
	v_pk_mul_f32 v[60:61], v[178:179], v[58:59] op_sel:[1,1] op_sel_hi:[0,1] neg_lo:[0,1]
	v_pk_fma_f32 v[58:59], v[178:179], v[58:59], v[60:61] op_sel_hi:[1,0,1]
	v_pk_mul_f32 v[60:61], v[46:47], v[58:59] op_sel:[1,1] op_sel_hi:[1,0] neg_lo:[1,0]
	v_pk_fma_f32 v[46:47], v[46:47], v[58:59], v[60:61] op_sel_hi:[0,1,1]
	ds_write_b64 v13, v[46:47] offset:33792
	v_pk_mul_f32 v[46:47], v[178:179], v[58:59] op_sel:[1,1] op_sel_hi:[0,1] neg_lo:[0,1]
	v_pk_fma_f32 v[46:47], v[178:179], v[58:59], v[46:47] op_sel_hi:[1,0,1]
	v_pk_mul_f32 v[58:59], v[66:67], v[46:47] op_sel:[1,1] op_sel_hi:[1,0] neg_lo:[1,0]
	v_pk_fma_f32 v[58:59], v[66:67], v[46:47], v[58:59] op_sel_hi:[0,1,1]
	ds_write_b64 v13, v[58:59] offset:38016
	v_pk_mul_f32 v[58:59], v[178:179], v[46:47] op_sel:[1,1] op_sel_hi:[0,1] neg_lo:[0,1]
	v_pk_fma_f32 v[46:47], v[178:179], v[46:47], v[58:59] op_sel_hi:[1,0,1]
	v_pk_mul_f32 v[58:59], v[50:51], v[46:47] op_sel:[1,1] op_sel_hi:[1,0] neg_lo:[1,0]
	v_pk_fma_f32 v[50:51], v[50:51], v[46:47], v[58:59] op_sel_hi:[0,1,1]
	ds_write_b64 v13, v[50:51] offset:42240
	v_pk_mul_f32 v[50:51], v[178:179], v[46:47] op_sel:[1,1] op_sel_hi:[0,1] neg_lo:[0,1]
	v_pk_fma_f32 v[46:47], v[178:179], v[46:47], v[50:51] op_sel_hi:[1,0,1]
	v_pk_mul_f32 v[50:51], v[78:79], v[46:47] op_sel:[1,1] op_sel_hi:[1,0] neg_lo:[1,0]
	v_pk_fma_f32 v[50:51], v[78:79], v[46:47], v[50:51] op_sel_hi:[0,1,1]
	ds_write_b64 v13, v[50:51] offset:46464
	v_pk_mul_f32 v[50:51], v[178:179], v[46:47] op_sel:[1,1] op_sel_hi:[0,1] neg_lo:[0,1]
	v_pk_fma_f32 v[46:47], v[178:179], v[46:47], v[50:51] op_sel_hi:[1,0,1]
	v_pk_mul_f32 v[50:51], v[40:41], v[46:47] op_sel:[1,1] op_sel_hi:[1,0] neg_lo:[1,0]
	v_pk_fma_f32 v[40:41], v[40:41], v[46:47], v[50:51] op_sel_hi:[0,1,1]
	ds_write_b64 v13, v[40:41] offset:50688
	v_pk_mul_f32 v[40:41], v[178:179], v[46:47] op_sel:[1,1] op_sel_hi:[0,1] neg_lo:[0,1]
	v_pk_fma_f32 v[40:41], v[178:179], v[46:47], v[40:41] op_sel_hi:[1,0,1]
	v_pk_mul_f32 v[46:47], v[74:75], v[40:41] op_sel:[1,1] op_sel_hi:[1,0] neg_lo:[1,0]
	v_pk_fma_f32 v[46:47], v[74:75], v[40:41], v[46:47] op_sel_hi:[0,1,1]
	ds_write_b64 v13, v[46:47] offset:54912
	v_pk_mul_f32 v[46:47], v[178:179], v[40:41] op_sel:[1,1] op_sel_hi:[0,1] neg_lo:[0,1]
	v_pk_fma_f32 v[40:41], v[178:179], v[40:41], v[46:47] op_sel_hi:[1,0,1]
	v_pk_mul_f32 v[46:47], v[44:45], v[40:41] op_sel:[1,1] op_sel_hi:[1,0] neg_lo:[1,0]
	v_pk_fma_f32 v[44:45], v[44:45], v[40:41], v[46:47] op_sel_hi:[0,1,1]
	ds_write_b64 v13, v[44:45] offset:59136
	v_pk_mul_f32 v[44:45], v[178:179], v[40:41] op_sel:[1,1] op_sel_hi:[0,1] neg_lo:[0,1]
	v_pk_fma_f32 v[40:41], v[178:179], v[40:41], v[44:45] op_sel_hi:[1,0,1]
	v_pk_mul_f32 v[44:45], v[68:69], v[40:41] op_sel:[1,1] op_sel_hi:[1,0] neg_lo:[1,0]
	v_pk_fma_f32 v[44:45], v[68:69], v[40:41], v[44:45] op_sel_hi:[0,1,1]
	ds_write_b64 v13, v[44:45] offset:63360
	v_pk_mul_f32 v[44:45], v[178:179], v[40:41] op_sel:[1,1] op_sel_hi:[0,1] neg_lo:[0,1]
	v_pk_fma_f32 v[40:41], v[178:179], v[40:41], v[44:45] op_sel_hi:[1,0,1]
	s_mov_b32 s44, s95
	v_sub_f32_e32 v10, v30, v31
	v_pk_mul_f32 v[30:31], v[40:41], s[44:45]
	v_pk_fma_f32 v[30:31], v[10:11], v[40:41], v[30:31] op_sel:[0,0,1] op_sel_hi:[0,1,0]
	v_add_u32_e32 v10, 0x10800, v13
	ds_write_b64 v10, v[30:31]
	v_pk_mul_f32 v[30:31], v[178:179], v[40:41] op_sel:[1,1] op_sel_hi:[0,1] neg_lo:[0,1]
	v_pk_fma_f32 v[30:31], v[178:179], v[40:41], v[30:31] op_sel_hi:[1,0,1]
	v_pk_mul_f32 v[40:41], v[54:55], v[30:31] op_sel:[1,1] op_sel_hi:[1,0] neg_lo:[1,0]
	v_add_u32_e32 v10, 0x11880, v13
	v_pk_fma_f32 v[40:41], v[54:55], v[30:31], v[40:41] op_sel_hi:[0,1,1]
	ds_write_b64 v10, v[40:41]
	v_pk_mul_f32 v[40:41], v[178:179], v[30:31] op_sel:[1,1] op_sel_hi:[0,1] neg_lo:[0,1]
	v_pk_fma_f32 v[30:31], v[178:179], v[30:31], v[40:41] op_sel_hi:[1,0,1]
	v_pk_mul_f32 v[40:41], v[36:37], v[30:31] op_sel:[1,1] op_sel_hi:[1,0] neg_lo:[1,0]
	v_add_u32_e32 v10, 0x12900, v13
	v_pk_fma_f32 v[36:37], v[36:37], v[30:31], v[40:41] op_sel_hi:[0,1,1]
	ds_write_b64 v10, v[36:37]
	v_pk_mul_f32 v[36:37], v[178:179], v[30:31] op_sel:[1,1] op_sel_hi:[0,1] neg_lo:[0,1]
	v_pk_fma_f32 v[30:31], v[178:179], v[30:31], v[36:37] op_sel_hi:[1,0,1]
	v_pk_mul_f32 v[36:37], v[56:57], v[30:31] op_sel:[1,1] op_sel_hi:[1,0] neg_lo:[1,0]
	v_add_u32_e32 v10, 0x13980, v13
	v_pk_fma_f32 v[36:37], v[56:57], v[30:31], v[36:37] op_sel_hi:[0,1,1]
	ds_write_b64 v10, v[36:37]
	v_pk_mul_f32 v[36:37], v[178:179], v[30:31] op_sel:[1,1] op_sel_hi:[0,1] neg_lo:[0,1]
	v_pk_fma_f32 v[30:31], v[178:179], v[30:31], v[36:37] op_sel_hi:[1,0,1]
	v_pk_mul_f32 v[36:37], v[26:27], v[30:31] op_sel:[1,1] op_sel_hi:[1,0] neg_lo:[1,0]
	v_add_u32_e32 v10, 0x14a00, v13
	v_pk_fma_f32 v[26:27], v[26:27], v[30:31], v[36:37] op_sel_hi:[0,1,1]
	ds_write_b64 v10, v[26:27]
	v_pk_mul_f32 v[26:27], v[178:179], v[30:31] op_sel:[1,1] op_sel_hi:[0,1] neg_lo:[0,1]
	v_pk_fma_f32 v[26:27], v[178:179], v[30:31], v[26:27] op_sel_hi:[1,0,1]
	v_pk_mul_f32 v[30:31], v[48:49], v[26:27] op_sel:[1,1] op_sel_hi:[1,0] neg_lo:[1,0]
	v_add_u32_e32 v10, 0x15a80, v13
	v_pk_fma_f32 v[30:31], v[48:49], v[26:27], v[30:31] op_sel_hi:[0,1,1]
	ds_write_b64 v10, v[30:31]
	v_pk_mul_f32 v[30:31], v[178:179], v[26:27] op_sel:[1,1] op_sel_hi:[0,1] neg_lo:[0,1]
	v_pk_fma_f32 v[26:27], v[178:179], v[26:27], v[30:31] op_sel_hi:[1,0,1]
	v_pk_mul_f32 v[30:31], v[28:29], v[26:27] op_sel:[1,1] op_sel_hi:[1,0] neg_lo:[1,0]
	v_add_u32_e32 v10, 0x16b00, v13
	v_pk_fma_f32 v[28:29], v[28:29], v[26:27], v[30:31] op_sel_hi:[0,1,1]
	ds_write_b64 v10, v[28:29]
	v_pk_mul_f32 v[28:29], v[178:179], v[26:27] op_sel:[1,1] op_sel_hi:[0,1] neg_lo:[0,1]
	v_pk_fma_f32 v[26:27], v[178:179], v[26:27], v[28:29] op_sel_hi:[1,0,1]
	v_pk_mul_f32 v[28:29], v[52:53], v[26:27] op_sel:[1,1] op_sel_hi:[1,0] neg_lo:[1,0]
	v_add_u32_e32 v10, 0x17b80, v13
	v_pk_fma_f32 v[28:29], v[52:53], v[26:27], v[28:29] op_sel_hi:[0,1,1]
	ds_write_b64 v10, v[28:29]
	v_pk_mul_f32 v[28:29], v[178:179], v[26:27] op_sel:[1,1] op_sel_hi:[0,1] neg_lo:[0,1]
	v_pk_fma_f32 v[26:27], v[178:179], v[26:27], v[28:29] op_sel_hi:[1,0,1]
	v_pk_mul_f32 v[28:29], v[20:21], v[26:27] op_sel:[1,1] op_sel_hi:[1,0] neg_lo:[1,0]
	v_add_u32_e32 v10, 0x18c00, v13
	v_pk_fma_f32 v[20:21], v[20:21], v[26:27], v[28:29] op_sel_hi:[0,1,1]
	ds_write_b64 v10, v[20:21]
	v_pk_mul_f32 v[20:21], v[178:179], v[26:27] op_sel:[1,1] op_sel_hi:[0,1] neg_lo:[0,1]
	v_pk_fma_f32 v[20:21], v[178:179], v[26:27], v[20:21] op_sel_hi:[1,0,1]
	v_pk_mul_f32 v[26:27], v[38:39], v[20:21] op_sel:[1,1] op_sel_hi:[1,0] neg_lo:[1,0]
	v_add_u32_e32 v10, 0x19c80, v13
	v_pk_fma_f32 v[26:27], v[38:39], v[20:21], v[26:27] op_sel_hi:[0,1,1]
	ds_write_b64 v10, v[26:27]
	v_pk_mul_f32 v[26:27], v[178:179], v[20:21] op_sel:[1,1] op_sel_hi:[0,1] neg_lo:[0,1]
	v_pk_fma_f32 v[20:21], v[178:179], v[20:21], v[26:27] op_sel_hi:[1,0,1]
	v_pk_mul_f32 v[26:27], v[24:25], v[20:21] op_sel:[1,1] op_sel_hi:[1,0] neg_lo:[1,0]
	v_add_u32_e32 v10, 0x1ad00, v13
	v_pk_fma_f32 v[24:25], v[24:25], v[20:21], v[26:27] op_sel_hi:[0,1,1]
	ds_write_b64 v10, v[24:25]
	v_pk_mul_f32 v[24:25], v[178:179], v[20:21] op_sel:[1,1] op_sel_hi:[0,1] neg_lo:[0,1]
	v_pk_fma_f32 v[20:21], v[178:179], v[20:21], v[24:25] op_sel_hi:[1,0,1]
	v_pk_mul_f32 v[24:25], v[42:43], v[20:21] op_sel:[1,1] op_sel_hi:[1,0] neg_lo:[1,0]
	v_add_u32_e32 v10, 0x1bd80, v13
	v_pk_fma_f32 v[24:25], v[42:43], v[20:21], v[24:25] op_sel_hi:[0,1,1]
	ds_write_b64 v10, v[24:25]
	v_pk_mul_f32 v[24:25], v[178:179], v[20:21] op_sel:[1,1] op_sel_hi:[0,1] neg_lo:[0,1]
	v_pk_fma_f32 v[20:21], v[178:179], v[20:21], v[24:25] op_sel_hi:[1,0,1]
	v_pk_mul_f32 v[24:25], v[14:15], v[20:21] op_sel:[1,1] op_sel_hi:[1,0] neg_lo:[1,0]
	v_add_u32_e32 v10, 0x1ce00, v13
	v_pk_fma_f32 v[14:15], v[14:15], v[20:21], v[24:25] op_sel_hi:[0,1,1]
	ds_write_b64 v10, v[14:15]
	v_pk_mul_f32 v[14:15], v[178:179], v[20:21] op_sel:[1,1] op_sel_hi:[0,1] neg_lo:[0,1]
	v_pk_fma_f32 v[14:15], v[178:179], v[20:21], v[14:15] op_sel_hi:[1,0,1]
	v_pk_mul_f32 v[20:21], v[34:35], v[14:15] op_sel:[1,1] op_sel_hi:[1,0] neg_lo:[1,0]
	v_add_u32_e32 v10, 0x1de80, v13
	v_pk_fma_f32 v[20:21], v[34:35], v[14:15], v[20:21] op_sel_hi:[0,1,1]
	ds_write_b64 v10, v[20:21]
	v_pk_mul_f32 v[20:21], v[178:179], v[14:15] op_sel:[1,1] op_sel_hi:[0,1] neg_lo:[0,1]
	v_pk_fma_f32 v[14:15], v[178:179], v[14:15], v[20:21] op_sel_hi:[1,0,1]
	v_pk_mul_f32 v[20:21], v[18:19], v[14:15] op_sel:[1,1] op_sel_hi:[1,0] neg_lo:[1,0]
	v_add_u32_e32 v10, 0x1ef00, v13
	v_pk_fma_f32 v[18:19], v[18:19], v[14:15], v[20:21] op_sel_hi:[0,1,1]
	ds_write_b64 v10, v[18:19]
	v_pk_mul_f32 v[18:19], v[178:179], v[14:15] op_sel:[1,1] op_sel_hi:[0,1] neg_lo:[0,1]
	v_pk_fma_f32 v[14:15], v[178:179], v[14:15], v[18:19] op_sel_hi:[1,0,1]
	v_pk_mul_f32 v[18:19], v[32:33], v[14:15] op_sel:[1,1] op_sel_hi:[1,0] neg_lo:[1,0]
	v_add_u32_e32 v10, 0x1ff80, v13
	v_pk_fma_f32 v[14:15], v[32:33], v[14:15], v[18:19] op_sel_hi:[0,1,1]
	ds_write_b64 v10, v[14:15]
	v_mov_b32_e32 v10, v174
	v_mov_b32_e32 v13, v172
	s_waitcnt lgkmcnt(0)
	s_barrier
	v_mov_b32_e32 v14, v180
	v_xad_u32 v30, v13, 3, v10
	v_lshl_add_u32 v73, v30, 3, 0
	v_xad_u32 v30, v13, 4, v10
	v_lshl_add_u32 v72, v30, 3, 0
	v_xad_u32 v30, v13, 5, v10
	v_lshl_add_u32 v71, v30, 3, 0
	v_xad_u32 v30, v13, 6, v10
	v_lshl_add_u32 v70, v30, 3, 0
	v_xad_u32 v30, v13, 7, v10
	v_lshl_add_u32 v69, v30, 3, 0
	v_xad_u32 v30, v13, 8, v10
	v_lshl_add_u32 v30, v30, 3, 0
	v_add_u32_e32 v68, 0x800, v30
	v_xad_u32 v30, v13, 9, v10
	v_lshl_add_u32 v30, v30, 3, 0
	v_add_u32_e32 v67, 0x800, v30
	v_xad_u32 v30, v13, 10, v10
	v_lshl_add_u32 v30, v30, 3, 0
	v_add_u32_e32 v66, 0x800, v30
	v_xad_u32 v30, v13, 11, v10
	v_lshl_add_u32 v30, v30, 3, 0
	v_add_u32_e32 v18, v13, v10
	v_add_u32_e32 v65, 0x800, v30
	v_xad_u32 v30, v13, 12, v10
	v_mov_b32_e32 v15, v181
	v_lshl_add_u32 v76, v18, 3, 0
	v_lshl_add_u32 v30, v30, 3, 0
	ds_read2_b64 v[18:21], v76 offset1:16
	ds_read2_b64 v[40:43], v68 offset1:16
	v_add_u32_e32 v64, 0x800, v30
	v_xad_u32 v30, v13, 13, v10
	v_xad_u32 v22, v13, 1, v10
	v_lshl_add_u32 v30, v30, 3, 0
	v_lshl_add_u32 v75, v22, 3, 0
	v_xad_u32 v26, v13, 2, v10
	v_add_u32_e32 v63, 0x800, v30
	v_xad_u32 v30, v13, 14, v10
	v_xad_u32 v10, v13, 15, v10
	ds_read2_b64 v[22:25], v75 offset0:32 offset1:48
	ds_read2_b64 v[48:51], v67 offset0:32 offset1:48
	v_lshl_add_u32 v30, v30, 3, 0
	v_lshl_add_u32 v10, v10, 3, 0
	v_lshl_add_u32 v74, v26, 3, 0
	v_add_u32_e32 v62, 0x800, v30
	v_add_u32_e32 v13, 0x800, v10
	v_mov_b32_e32 v10, v1
	ds_read2_b64 v[26:29], v74 offset0:64 offset1:80
	ds_read2_b64 v[58:61], v73 offset0:96 offset1:112
	ds_read2_b64 v[78:81], v72 offset0:128 offset1:144
	ds_read2_b64 v[82:85], v71 offset0:160 offset1:176
	ds_read2_b64 v[86:89], v70 offset0:192 offset1:208
	ds_read2_b64 v[90:93], v69 offset0:224 offset1:240
	ds_read2_b64 v[54:57], v66 offset0:64 offset1:80
	ds_read2_b64 v[94:97], v65 offset0:96 offset1:112
	ds_read2_b64 v[98:101], v64 offset0:128 offset1:144
	ds_read2_b64 v[102:105], v63 offset0:160 offset1:176
	ds_read2_b64 v[106:109], v62 offset0:192 offset1:208
	ds_read2_b64 v[110:113], v13 offset0:224 offset1:240
	s_waitcnt lgkmcnt(14)
	v_pk_add_f32 v[114:115], v[18:19], v[40:41]
	v_pk_add_f32 v[40:41], v[18:19], v[40:41] neg_lo:[0,1] neg_hi:[0,1]
	v_pk_add_f32 v[18:19], v[20:21], v[42:43]
	v_pk_add_f32 v[20:21], v[20:21], v[42:43] neg_lo:[0,1] neg_hi:[0,1]
	v_mov_b32_e32 v30, v164
	v_mov_b32_e32 v32, v165
	v_mov_b32_e32 v34, v166
	v_mov_b32_e32 v10, v167
	v_mov_b32_e32 v38, v168
	v_mov_b32_e32 v36, v169
	v_mov_b32_e32 v46, v170
	v_mov_b32_e32 v31, v171
	v_pk_mul_f32 v[42:43], v[20:21], v[46:47] op_sel:[1,0] op_sel_hi:[0,0] neg_lo:[1,1] neg_hi:[0,1]
	s_mov_b32 s14, s95
	v_pk_fma_f32 v[44:45], v[20:21], v[30:31], v[42:43] op_sel_hi:[1,0,1]
	s_waitcnt lgkmcnt(12)
	v_pk_add_f32 v[20:21], v[22:23], v[48:49]
	v_pk_add_f32 v[22:23], v[22:23], v[48:49] neg_lo:[0,1] neg_hi:[0,1]
	s_mov_b32 s15, s94
	v_pk_mul_f32 v[42:43], v[22:23], v[36:37] op_sel:[1,0] op_sel_hi:[0,0] neg_lo:[1,1] neg_hi:[0,1]
	v_pk_fma_f32 v[48:49], v[22:23], v[32:33], v[42:43] op_sel_hi:[1,0,1]
	v_pk_add_f32 v[22:23], v[24:25], v[50:51]
	v_pk_add_f32 v[24:25], v[24:25], v[50:51] neg_lo:[0,1] neg_hi:[0,1]
	v_pk_mul_f32 v[42:43], v[24:25], v[38:39] op_sel:[1,0] op_sel_hi:[0,0] neg_lo:[1,1] neg_hi:[0,1]
	v_pk_fma_f32 v[52:53], v[24:25], v[34:35], v[42:43] op_sel_hi:[1,0,1]
	s_waitcnt lgkmcnt(5)
	v_pk_add_f32 v[24:25], v[26:27], v[54:55]
	v_pk_add_f32 v[26:27], v[26:27], v[54:55] neg_lo:[0,1] neg_hi:[0,1]
	v_pk_mul_f32 v[42:43], v[26:27], v[10:11] op_sel:[1,0] op_sel_hi:[0,0] neg_lo:[1,1] neg_hi:[0,1]
	v_pk_fma_f32 v[54:55], v[26:27], v[10:11], v[42:43] op_sel_hi:[1,0,1]
	v_pk_add_f32 v[26:27], v[28:29], v[56:57]
	v_pk_add_f32 v[28:29], v[28:29], v[56:57] neg_lo:[0,1] neg_hi:[0,1]
	v_pk_mul_f32 v[42:43], v[28:29], v[38:39] op_sel_hi:[1,0]
	v_pk_fma_f32 v[56:57], v[28:29], v[34:35], v[42:43] op_sel:[1,0,0] op_sel_hi:[0,0,1] neg_lo:[1,1,0] neg_hi:[0,1,0]
	s_waitcnt lgkmcnt(4)
	v_pk_add_f32 v[42:43], v[58:59], v[94:95] neg_lo:[0,1] neg_hi:[0,1]
	v_pk_add_f32 v[28:29], v[58:59], v[94:95]
	v_pk_mul_f32 v[50:51], v[42:43], v[36:37] op_sel_hi:[1,0]
	v_pk_fma_f32 v[58:59], v[42:43], v[32:33], v[50:51] op_sel:[1,0,0] op_sel_hi:[0,0,1] neg_lo:[1,1,0] neg_hi:[0,1,0]
	v_pk_add_f32 v[50:51], v[60:61], v[96:97] neg_lo:[0,1] neg_hi:[0,1]
	v_pk_add_f32 v[42:43], v[60:61], v[96:97]
	v_pk_mul_f32 v[60:61], v[50:51], v[46:47] op_sel_hi:[1,0]
	v_xor_b32_e32 v94, 0x80000000, v51
	v_mov_b32_e32 v95, v50
	s_waitcnt lgkmcnt(3)
	v_pk_add_f32 v[50:51], v[78:79], v[98:99]
	v_pk_add_f32 v[78:79], v[78:79], v[98:99] neg_lo:[0,1] neg_hi:[0,1]
	v_pk_fma_f32 v[60:61], v[94:95], v[30:31], v[60:61] op_sel_hi:[1,0,1] neg_lo:[0,1,0] neg_hi:[0,1,0]
	v_xor_b32_e32 v95, 0x80000000, v78
	v_mov_b32_e32 v94, v79
	v_pk_add_f32 v[78:79], v[80:81], v[100:101]
	v_pk_add_f32 v[80:81], v[80:81], v[100:101] neg_lo:[0,1] neg_hi:[0,1]
	v_pk_mul_f32 v[96:97], v[80:81], v[46:47] op_sel_hi:[1,0] neg_lo:[0,1] neg_hi:[0,1]
	v_pk_fma_f32 v[80:81], v[80:81], v[30:31], v[96:97] op_sel:[1,0,0] op_sel_hi:[0,0,1] neg_lo:[1,1,0] neg_hi:[0,1,0]
	s_waitcnt lgkmcnt(2)
	v_pk_add_f32 v[96:97], v[82:83], v[102:103]
	v_pk_add_f32 v[82:83], v[82:83], v[102:103] neg_lo:[0,1] neg_hi:[0,1]
	v_pk_mul_f32 v[98:99], v[82:83], v[36:37] op_sel_hi:[1,0] neg_lo:[0,1] neg_hi:[0,1]
	v_pk_fma_f32 v[82:83], v[82:83], v[32:33], v[98:99] op_sel:[1,0,0] op_sel_hi:[0,0,1] neg_lo:[1,1,0] neg_hi:[0,1,0]
	v_pk_add_f32 v[98:99], v[84:85], v[104:105]
	v_pk_add_f32 v[84:85], v[84:85], v[104:105] neg_lo:[0,1] neg_hi:[0,1]
	v_pk_mul_f32 v[100:101], v[84:85], v[38:39] op_sel_hi:[1,0] neg_lo:[0,1] neg_hi:[0,1]
	v_pk_fma_f32 v[84:85], v[84:85], v[34:35], v[100:101] op_sel:[1,0,0] op_sel_hi:[0,0,1] neg_lo:[1,1,0] neg_hi:[0,1,0]
	s_waitcnt lgkmcnt(1)
	v_pk_add_f32 v[100:101], v[86:87], v[106:107]
	v_pk_add_f32 v[86:87], v[86:87], v[106:107] neg_lo:[0,1] neg_hi:[0,1]
	v_pk_mul_f32 v[102:103], v[86:87], v[10:11] op_sel:[1,0] op_sel_hi:[0,0] neg_lo:[1,1] neg_hi:[0,1]
	v_pk_fma_f32 v[86:87], v[86:87], v[10:11], v[102:103] op_sel_hi:[1,0,1] neg_lo:[0,1,0] neg_hi:[0,1,0]
	v_pk_add_f32 v[102:103], v[88:89], v[108:109]
	v_pk_add_f32 v[88:89], v[88:89], v[108:109] neg_lo:[0,1] neg_hi:[0,1]
	v_pk_mul_f32 v[38:39], v[88:89], v[38:39] op_sel:[1,0] op_sel_hi:[0,0] neg_lo:[1,1] neg_hi:[0,1]
	v_pk_fma_f32 v[88:89], v[88:89], v[34:35], v[38:39] op_sel_hi:[1,0,1] neg_lo:[0,1,0] neg_hi:[0,1,0]
	s_waitcnt lgkmcnt(0)
	v_pk_add_f32 v[38:39], v[90:91], v[110:111] neg_lo:[0,1] neg_hi:[0,1]
	v_pk_add_f32 v[34:35], v[90:91], v[110:111]
	v_pk_mul_f32 v[90:91], v[38:39], v[36:37] op_sel:[1,0] op_sel_hi:[0,0] neg_lo:[1,1] neg_hi:[0,1]
	v_pk_fma_f32 v[90:91], v[38:39], v[32:33], v[90:91] op_sel_hi:[1,0,1] neg_lo:[0,1,0] neg_hi:[0,1,0]
	v_pk_add_f32 v[38:39], v[92:93], v[112:113]
	v_pk_add_f32 v[92:93], v[92:93], v[112:113] neg_lo:[0,1] neg_hi:[0,1]
	v_pk_mul_f32 v[46:47], v[92:93], v[46:47] op_sel:[1,0] op_sel_hi:[0,0] neg_lo:[1,1] neg_hi:[0,1]
	v_pk_fma_f32 v[92:93], v[92:93], v[30:31], v[46:47] op_sel_hi:[1,0,1] neg_lo:[0,1,0] neg_hi:[0,1,0]
	v_pk_add_f32 v[46:47], v[18:19], v[78:79]
	v_pk_add_f32 v[18:19], v[18:19], v[78:79] neg_lo:[0,1] neg_hi:[0,1]
	v_pk_add_f32 v[30:31], v[114:115], v[50:51]
	v_pk_mul_f32 v[78:79], v[18:19], v[36:37] op_sel:[1,0] op_sel_hi:[0,0] neg_lo:[1,1] neg_hi:[0,1]
	v_pk_add_f32 v[50:51], v[114:115], v[50:51] neg_lo:[0,1] neg_hi:[0,1]
	v_pk_fma_f32 v[78:79], v[18:19], v[32:33], v[78:79] op_sel_hi:[1,0,1]
	v_pk_add_f32 v[18:19], v[20:21], v[96:97]
	v_pk_add_f32 v[20:21], v[20:21], v[96:97] neg_lo:[0,1] neg_hi:[0,1]
	v_pk_mul_f32 v[96:97], v[20:21], v[10:11] op_sel:[1,0] op_sel_hi:[0,0] neg_lo:[1,1] neg_hi:[0,1]
	v_pk_fma_f32 v[20:21], v[20:21], v[10:11], v[96:97] op_sel_hi:[1,0,1]
	v_pk_add_f32 v[96:97], v[22:23], v[98:99]
	v_pk_add_f32 v[22:23], v[22:23], v[98:99] neg_lo:[0,1] neg_hi:[0,1]
	v_pk_mul_f32 v[98:99], v[22:23], v[36:37] op_sel_hi:[1,0]
	v_xor_b32_e32 v104, 0x80000000, v23
	v_mov_b32_e32 v105, v22
	v_pk_add_f32 v[22:23], v[24:25], v[100:101]
	v_pk_add_f32 v[24:25], v[24:25], v[100:101] neg_lo:[0,1] neg_hi:[0,1]
	v_pk_fma_f32 v[98:99], v[104:105], v[32:33], v[98:99] op_sel_hi:[1,0,1] neg_lo:[0,1,0] neg_hi:[0,1,0]
	v_xor_b32_e32 v101, 0x80000000, v24
	v_mov_b32_e32 v100, v25
	v_pk_add_f32 v[24:25], v[26:27], v[102:103]
	v_pk_add_f32 v[26:27], v[26:27], v[102:103] neg_lo:[0,1] neg_hi:[0,1]
	v_pk_mul_f32 v[102:103], v[26:27], v[36:37] op_sel_hi:[1,0] neg_lo:[0,1] neg_hi:[0,1]
	v_xor_b32_e32 v104, 0x80000000, v27
	v_mov_b32_e32 v105, v26
	v_pk_add_f32 v[26:27], v[28:29], v[34:35]
	v_pk_add_f32 v[28:29], v[28:29], v[34:35] neg_lo:[0,1] neg_hi:[0,1]
	v_pk_fma_f32 v[102:103], v[104:105], v[32:33], v[102:103] op_sel_hi:[1,0,1] neg_lo:[0,1,0] neg_hi:[0,1,0]
	v_pk_mul_f32 v[34:35], v[28:29], v[10:11] op_sel:[1,0] op_sel_hi:[0,0] neg_lo:[1,1] neg_hi:[0,1]
	v_pk_add_f32 v[104:105], v[30:31], v[22:23] neg_lo:[0,1] neg_hi:[0,1]
	v_pk_fma_f32 v[28:29], v[28:29], v[10:11], v[34:35] op_sel_hi:[1,0,1] neg_lo:[0,1,0] neg_hi:[0,1,0]
	v_pk_add_f32 v[34:35], v[42:43], v[38:39]
	v_pk_add_f32 v[38:39], v[42:43], v[38:39] neg_lo:[0,1] neg_hi:[0,1]
	v_pk_mul_f32 v[42:43], v[38:39], v[36:37] op_sel:[1,0] op_sel_hi:[0,0] neg_lo:[1,1] neg_hi:[0,1]
	v_pk_fma_f32 v[42:43], v[38:39], v[32:33], v[42:43] op_sel_hi:[1,0,1] neg_lo:[0,1,0] neg_hi:[0,1,0]
	v_pk_add_f32 v[38:39], v[30:31], v[22:23]
	v_pk_add_f32 v[22:23], v[46:47], v[24:25]
	v_pk_add_f32 v[24:25], v[46:47], v[24:25] neg_lo:[0,1] neg_hi:[0,1]
	v_pk_mul_f32 v[30:31], v[24:25], v[10:11] op_sel:[1,0] op_sel_hi:[0,0] neg_lo:[1,1] neg_hi:[0,1]
	v_pk_fma_f32 v[24:25], v[24:25], v[10:11], v[30:31] op_sel_hi:[1,0,1]
	v_pk_add_f32 v[30:31], v[18:19], v[26:27]
	v_pk_add_f32 v[18:19], v[18:19], v[26:27] neg_lo:[0,1] neg_hi:[0,1]
	v_xor_b32_e32 v27, 0x80000000, v18
	v_mov_b32_e32 v26, v19
	v_pk_add_f32 v[18:19], v[96:97], v[34:35]
	v_pk_add_f32 v[34:35], v[96:97], v[34:35] neg_lo:[0,1] neg_hi:[0,1]
	v_pk_mul_f32 v[46:47], v[34:35], v[10:11] op_sel:[1,0] op_sel_hi:[0,0] neg_lo:[1,1] neg_hi:[0,1]
	v_pk_fma_f32 v[34:35], v[34:35], v[10:11], v[46:47] op_sel_hi:[1,0,1] neg_lo:[0,1,0] neg_hi:[0,1,0]
	v_pk_add_f32 v[46:47], v[38:39], v[30:31]
	v_pk_add_f32 v[38:39], v[38:39], v[30:31] neg_lo:[0,1] neg_hi:[0,1]
	v_pk_add_f32 v[30:31], v[22:23], v[18:19]
	v_pk_add_f32 v[18:19], v[22:23], v[18:19] neg_lo:[0,1] neg_hi:[0,1]
	v_pk_add_f32 v[96:97], v[46:47], v[30:31]
	v_xor_b32_e32 v23, 0x80000000, v18
	v_mov_b32_e32 v22, v19
	v_pk_add_f32 v[18:19], v[104:105], v[26:27]
	v_pk_add_f32 v[104:105], v[104:105], v[26:27] neg_lo:[0,1] neg_hi:[0,1]
	v_pk_add_f32 v[26:27], v[24:25], v[34:35]
	v_pk_add_f32 v[24:25], v[24:25], v[34:35] neg_lo:[0,1] neg_hi:[0,1]
	v_pk_add_f32 v[30:31], v[46:47], v[30:31] neg_lo:[0,1] neg_hi:[0,1]
	v_xor_b32_e32 v35, 0x80000000, v24
	v_mov_b32_e32 v34, v25
	v_pk_add_f32 v[24:25], v[50:51], v[100:101]
	v_pk_add_f32 v[100:101], v[50:51], v[100:101] neg_lo:[0,1] neg_hi:[0,1]
	v_pk_add_f32 v[50:51], v[78:79], v[102:103] neg_lo:[0,1] neg_hi:[0,1]
	v_pk_add_f32 v[46:47], v[38:39], v[22:23]
	v_pk_add_f32 v[22:23], v[38:39], v[22:23] neg_lo:[0,1] neg_hi:[0,1]
	v_pk_add_f32 v[106:107], v[18:19], v[26:27]
	v_pk_add_f32 v[26:27], v[18:19], v[26:27] neg_lo:[0,1] neg_hi:[0,1]
	v_pk_add_f32 v[38:39], v[104:105], v[34:35]
	v_pk_add_f32 v[18:19], v[104:105], v[34:35] neg_lo:[0,1] neg_hi:[0,1]
	v_pk_add_f32 v[34:35], v[78:79], v[102:103]
	v_pk_mul_f32 v[78:79], v[10:11], v[50:51] op_sel:[0,1] op_sel_hi:[0,0] neg_lo:[1,1] neg_hi:[1,0]
	v_pk_fma_f32 v[78:79], v[10:11], v[50:51], v[78:79] op_sel_hi:[0,1,1]
	v_pk_add_f32 v[50:51], v[20:21], v[28:29]
	v_pk_add_f32 v[20:21], v[20:21], v[28:29] neg_lo:[0,1] neg_hi:[0,1]
	v_xor_b32_e32 v29, 0x80000000, v20
	v_mov_b32_e32 v28, v21
	v_pk_add_f32 v[20:21], v[98:99], v[42:43]
	v_pk_add_f32 v[42:43], v[98:99], v[42:43] neg_lo:[0,1] neg_hi:[0,1]
	v_pk_mul_f32 v[98:99], v[10:11], v[42:43] op_sel:[0,1] op_sel_hi:[0,0] neg_lo:[1,1] neg_hi:[1,0]
	v_pk_fma_f32 v[42:43], v[10:11], v[42:43], v[98:99] op_sel_hi:[0,1,1] neg_lo:[1,0,0] neg_hi:[1,0,0]
	v_pk_add_f32 v[98:99], v[24:25], v[50:51]
	v_pk_add_f32 v[24:25], v[24:25], v[50:51] neg_lo:[0,1] neg_hi:[0,1]
	v_pk_add_f32 v[50:51], v[34:35], v[20:21]
	v_pk_add_f32 v[20:21], v[34:35], v[20:21] neg_lo:[0,1] neg_hi:[0,1]
	v_pk_add_f32 v[104:105], v[98:99], v[50:51]
	v_xor_b32_e32 v103, 0x80000000, v20
	v_mov_b32_e32 v102, v21
	v_pk_add_f32 v[34:35], v[98:99], v[50:51] neg_lo:[0,1] neg_hi:[0,1]
	v_pk_add_f32 v[20:21], v[100:101], v[28:29]
	v_pk_add_f32 v[98:99], v[100:101], v[28:29] neg_lo:[0,1] neg_hi:[0,1]
	v_pk_add_f32 v[28:29], v[78:79], v[42:43]
	v_pk_add_f32 v[42:43], v[78:79], v[42:43] neg_lo:[0,1] neg_hi:[0,1]
	v_pk_add_f32 v[100:101], v[20:21], v[28:29]
	v_xor_b32_e32 v79, 0x80000000, v42
	v_mov_b32_e32 v78, v43
	v_pk_add_f32 v[28:29], v[20:21], v[28:29] neg_lo:[0,1] neg_hi:[0,1]
	v_pk_add_f32 v[42:43], v[98:99], v[78:79]
	v_pk_add_f32 v[20:21], v[98:99], v[78:79] neg_lo:[0,1] neg_hi:[0,1]
	v_pk_add_f32 v[78:79], v[40:41], v[94:95]
	v_pk_add_f32 v[94:95], v[40:41], v[94:95] neg_lo:[0,1] neg_hi:[0,1]
	v_pk_add_f32 v[40:41], v[44:45], v[80:81]
	v_pk_add_f32 v[44:45], v[44:45], v[80:81] neg_lo:[0,1] neg_hi:[0,1]
	v_pk_add_f32 v[50:51], v[24:25], v[102:103]
	v_pk_mul_f32 v[80:81], v[36:37], v[44:45] op_sel:[0,1] op_sel_hi:[0,0] neg_lo:[1,1] neg_hi:[1,0]
	v_pk_fma_f32 v[44:45], v[32:33], v[44:45], v[80:81] op_sel_hi:[0,1,1]
	v_pk_add_f32 v[80:81], v[48:49], v[82:83]
	v_pk_add_f32 v[48:49], v[48:49], v[82:83] neg_lo:[0,1] neg_hi:[0,1]
	v_pk_add_f32 v[24:25], v[24:25], v[102:103] neg_lo:[0,1] neg_hi:[0,1]
	v_pk_mul_f32 v[82:83], v[10:11], v[48:49] op_sel:[0,1] op_sel_hi:[0,0] neg_lo:[1,1] neg_hi:[1,0]
	v_pk_fma_f32 v[82:83], v[10:11], v[48:49], v[82:83] op_sel_hi:[0,1,1]
	v_pk_add_f32 v[48:49], v[52:53], v[84:85]
	v_pk_add_f32 v[52:53], v[52:53], v[84:85] neg_lo:[0,1] neg_hi:[0,1]
	v_pk_mul_f32 v[84:85], v[32:33], v[52:53] op_sel:[0,1] op_sel_hi:[0,0] neg_lo:[1,1] neg_hi:[1,0]
	v_pk_fma_f32 v[52:53], v[36:37], v[52:53], v[84:85] op_sel_hi:[0,1,1]
	v_pk_add_f32 v[84:85], v[54:55], v[86:87]
	v_pk_add_f32 v[54:55], v[54:55], v[86:87] neg_lo:[0,1] neg_hi:[0,1]
	v_xor_b32_e32 v87, 0x80000000, v54
	v_mov_b32_e32 v86, v55
	v_pk_add_f32 v[54:55], v[56:57], v[88:89]
	v_pk_add_f32 v[56:57], v[56:57], v[88:89] neg_lo:[0,1] neg_hi:[0,1]
	v_pk_mul_f32 v[88:89], v[32:33], v[56:57] op_sel:[0,1] op_sel_hi:[0,0] neg_lo:[1,1] neg_hi:[1,0]
	v_pk_fma_f32 v[56:57], v[36:37], v[56:57], v[88:89] op_sel_hi:[0,1,1] neg_lo:[1,0,0] neg_hi:[1,0,0]
	v_pk_add_f32 v[88:89], v[58:59], v[90:91]
	v_pk_add_f32 v[58:59], v[58:59], v[90:91] neg_lo:[0,1] neg_hi:[0,1]
	v_pk_mul_f32 v[90:91], v[10:11], v[58:59] op_sel:[0,1] op_sel_hi:[0,0] neg_lo:[1,1] neg_hi:[1,0]
	v_pk_fma_f32 v[58:59], v[10:11], v[58:59], v[90:91] op_sel_hi:[0,1,1] neg_lo:[1,0,0] neg_hi:[1,0,0]
	v_pk_add_f32 v[90:91], v[60:61], v[92:93]
	v_pk_add_f32 v[60:61], v[60:61], v[92:93] neg_lo:[0,1] neg_hi:[0,1]
	v_pk_mul_f32 v[36:37], v[36:37], v[60:61] op_sel:[0,1] op_sel_hi:[0,0] neg_lo:[1,1] neg_hi:[1,0]
	v_pk_fma_f32 v[36:37], v[32:33], v[60:61], v[36:37] op_sel_hi:[0,1,1] neg_lo:[1,0,0] neg_hi:[1,0,0]
	v_pk_add_f32 v[32:33], v[78:79], v[84:85]
	v_pk_add_f32 v[60:61], v[78:79], v[84:85] neg_lo:[0,1] neg_hi:[0,1]
	v_pk_add_f32 v[78:79], v[54:55], v[40:41]
	v_pk_add_f32 v[40:41], v[40:41], v[54:55] neg_lo:[0,1] neg_hi:[0,1]
	v_pk_mul_f32 v[54:55], v[10:11], v[40:41] op_sel:[0,1] op_sel_hi:[0,0] neg_lo:[1,1] neg_hi:[1,0]
	v_pk_fma_f32 v[54:55], v[10:11], v[40:41], v[54:55] op_sel_hi:[0,1,1]
	v_pk_add_f32 v[40:41], v[80:81], v[88:89]
	v_pk_add_f32 v[80:81], v[80:81], v[88:89] neg_lo:[0,1] neg_hi:[0,1]
	v_xor_b32_e32 v85, 0x80000000, v80
	v_mov_b32_e32 v84, v81
	v_pk_add_f32 v[80:81], v[48:49], v[90:91]
	v_pk_add_f32 v[48:49], v[48:49], v[90:91] neg_lo:[0,1] neg_hi:[0,1]
	v_pk_add_f32 v[90:91], v[78:79], v[80:81]
	v_pk_mul_f32 v[88:89], v[10:11], v[48:49] op_sel:[0,1] op_sel_hi:[0,0] neg_lo:[1,1] neg_hi:[1,0]
	v_pk_fma_f32 v[48:49], v[10:11], v[48:49], v[88:89] op_sel_hi:[0,1,1] neg_lo:[1,0,0] neg_hi:[1,0,0]
	v_pk_add_f32 v[88:89], v[32:33], v[40:41]
	v_pk_add_f32 v[32:33], v[32:33], v[40:41] neg_lo:[0,1] neg_hi:[0,1]
	v_pk_add_f32 v[40:41], v[78:79], v[80:81] neg_lo:[0,1] neg_hi:[0,1]
	v_pk_add_f32 v[80:81], v[88:89], v[90:91] neg_lo:[0,1] neg_hi:[0,1]
	v_pk_add_f32 v[92:93], v[32:33], v[40:41] op_sel:[0,1] op_sel_hi:[1,0] neg_hi:[0,1]
	v_pk_add_f32 v[40:41], v[32:33], v[40:41] op_sel:[0,1] op_sel_hi:[1,0] neg_lo:[0,1]
	v_pk_add_f32 v[78:79], v[54:55], v[48:49]
	v_pk_add_f32 v[48:49], v[54:55], v[48:49] neg_lo:[0,1] neg_hi:[0,1]
	v_pk_add_f32 v[32:33], v[60:61], v[84:85]
	v_pk_add_f32 v[60:61], v[60:61], v[84:85] neg_lo:[0,1] neg_hi:[0,1]
	v_xor_b32_e32 v55, 0x80000000, v48
	v_mov_b32_e32 v54, v49
	v_pk_add_f32 v[84:85], v[32:33], v[78:79]
	v_pk_add_f32 v[48:49], v[32:33], v[78:79] neg_lo:[0,1] neg_hi:[0,1]
	v_pk_add_f32 v[78:79], v[60:61], v[54:55]
	v_pk_add_f32 v[32:33], v[60:61], v[54:55] neg_lo:[0,1] neg_hi:[0,1]
	v_pk_add_f32 v[54:55], v[94:95], v[86:87]
	v_pk_add_f32 v[60:61], v[94:95], v[86:87] neg_lo:[0,1] neg_hi:[0,1]
	v_pk_add_f32 v[86:87], v[56:57], v[44:45]
	v_pk_add_f32 v[44:45], v[44:45], v[56:57] neg_lo:[0,1] neg_hi:[0,1]
	v_pk_add_f32 v[88:89], v[88:89], v[90:91]
	v_pk_mul_f32 v[56:57], v[10:11], v[44:45] op_sel:[0,1] op_sel_hi:[0,0] neg_lo:[1,1] neg_hi:[1,0]
	v_pk_fma_f32 v[56:57], v[10:11], v[44:45], v[56:57] op_sel_hi:[0,1,1]
	v_pk_add_f32 v[44:45], v[82:83], v[58:59]
	v_pk_add_f32 v[58:59], v[82:83], v[58:59] neg_lo:[0,1] neg_hi:[0,1]
	v_xor_b32_e32 v83, 0x80000000, v58
	v_mov_b32_e32 v82, v59
	v_pk_add_f32 v[58:59], v[52:53], v[36:37]
	v_pk_add_f32 v[36:37], v[52:53], v[36:37] neg_lo:[0,1] neg_hi:[0,1]
	v_pk_mul_f32 v[52:53], v[10:11], v[36:37] op_sel:[0,1] op_sel_hi:[0,0] neg_lo:[1,1] neg_hi:[1,0]
	v_pk_fma_f32 v[36:37], v[10:11], v[36:37], v[52:53] op_sel_hi:[0,1,1] neg_lo:[1,0,0] neg_hi:[1,0,0]
	v_pk_add_f32 v[52:53], v[54:55], v[44:45]
	v_pk_add_f32 v[44:45], v[54:55], v[44:45] neg_lo:[0,1] neg_hi:[0,1]
	v_pk_add_f32 v[54:55], v[86:87], v[58:59]
	v_pk_add_f32 v[58:59], v[86:87], v[58:59] neg_lo:[0,1] neg_hi:[0,1]
	v_xor_b32_e32 v87, 0x80000000, v58
	v_mov_b32_e32 v86, v59
	v_pk_add_f32 v[58:59], v[52:53], v[54:55]
	v_pk_add_f32 v[54:55], v[52:53], v[54:55] neg_lo:[0,1] neg_hi:[0,1]
	v_pk_add_f32 v[52:53], v[60:61], v[82:83]
	v_pk_add_f32 v[60:61], v[60:61], v[82:83] neg_lo:[0,1] neg_hi:[0,1]
	v_pk_add_f32 v[82:83], v[56:57], v[36:37]
	v_pk_add_f32 v[36:37], v[56:57], v[36:37] neg_lo:[0,1] neg_hi:[0,1]
	v_pk_add_f32 v[94:95], v[44:45], v[86:87]
	v_pk_add_f32 v[44:45], v[44:45], v[86:87] neg_lo:[0,1] neg_hi:[0,1]
	v_pk_add_f32 v[86:87], v[52:53], v[82:83]
	v_pk_add_f32 v[52:53], v[52:53], v[82:83] neg_lo:[0,1] neg_hi:[0,1]
	v_pk_add_f32 v[82:83], v[60:61], v[36:37] op_sel:[0,1] op_sel_hi:[1,0] neg_hi:[0,1]
	v_pk_add_f32 v[36:37], v[60:61], v[36:37] op_sel:[0,1] op_sel_hi:[1,0] neg_lo:[0,1]
	v_pk_fma_f32 v[60:61], v[14:15], s[90:91], v[14:15] op_sel:[1,0,0] op_sel_hi:[0,1,1]
	v_pk_mul_f32 v[56:57], v[96:97], s[14:15] op_sel:[1,0] neg_lo:[1,0]
	v_pk_mul_f32 v[90:91], v[60:61], v[88:89] op_sel:[1,1] op_sel_hi:[0,1] neg_lo:[0,1]
	v_pk_fma_f32 v[56:57], v[96:97], s[94:95], v[56:57] op_sel_hi:[0,1,1]
	v_pk_fma_f32 v[88:89], v[60:61], v[88:89], v[90:91] op_sel_hi:[1,0,1]
	ds_write2_b64 v76, v[56:57], v[88:89] offset1:16
	v_pk_mul_f32 v[56:57], v[14:15], v[60:61] op_sel:[1,1] op_sel_hi:[0,1] neg_lo:[0,1]
	v_pk_fma_f32 v[56:57], v[14:15], v[60:61], v[56:57] op_sel_hi:[1,0,1]
	v_pk_mul_f32 v[60:61], v[56:57], v[104:105] op_sel:[1,1] op_sel_hi:[0,1] neg_lo:[0,1]
	v_pk_mul_f32 v[76:77], v[14:15], v[56:57] op_sel:[1,1] op_sel_hi:[0,1] neg_lo:[0,1]
	v_pk_fma_f32 v[60:61], v[56:57], v[104:105], v[60:61] op_sel_hi:[1,0,1]
	v_pk_fma_f32 v[56:57], v[14:15], v[56:57], v[76:77] op_sel_hi:[1,0,1]
	v_pk_mul_f32 v[76:77], v[56:57], v[58:59] op_sel:[1,1] op_sel_hi:[0,1] neg_lo:[0,1]
	v_pk_fma_f32 v[58:59], v[56:57], v[58:59], v[76:77] op_sel_hi:[1,0,1]
	ds_write2_b64 v75, v[60:61], v[58:59] offset0:32 offset1:48
	v_pk_mul_f32 v[58:59], v[14:15], v[56:57] op_sel:[1,1] op_sel_hi:[0,1] neg_lo:[0,1]
	v_pk_fma_f32 v[56:57], v[14:15], v[56:57], v[58:59] op_sel_hi:[1,0,1]
	v_pk_mul_f32 v[58:59], v[56:57], v[106:107] op_sel:[1,1] op_sel_hi:[0,1] neg_lo:[0,1]
	v_pk_mul_f32 v[60:61], v[14:15], v[56:57] op_sel:[1,1] op_sel_hi:[0,1] neg_lo:[0,1]
	v_pk_fma_f32 v[58:59], v[56:57], v[106:107], v[58:59] op_sel_hi:[1,0,1]
	v_pk_fma_f32 v[56:57], v[14:15], v[56:57], v[60:61] op_sel_hi:[1,0,1]
	v_pk_mul_f32 v[60:61], v[56:57], v[84:85] op_sel:[1,1] op_sel_hi:[0,1] neg_lo:[0,1]
	v_pk_fma_f32 v[60:61], v[56:57], v[84:85], v[60:61] op_sel_hi:[1,0,1]
	ds_write2_b64 v74, v[58:59], v[60:61] offset0:64 offset1:80
	v_pk_mul_f32 v[58:59], v[14:15], v[56:57] op_sel:[1,1] op_sel_hi:[0,1] neg_lo:[0,1]
	v_pk_fma_f32 v[56:57], v[14:15], v[56:57], v[58:59] op_sel_hi:[1,0,1]
	v_pk_mul_f32 v[58:59], v[56:57], v[100:101] op_sel:[1,1] op_sel_hi:[0,1] neg_lo:[0,1]
	v_pk_mul_f32 v[60:61], v[14:15], v[56:57] op_sel:[1,1] op_sel_hi:[0,1] neg_lo:[0,1]
	v_pk_fma_f32 v[58:59], v[56:57], v[100:101], v[58:59] op_sel_hi:[1,0,1]
	v_pk_fma_f32 v[56:57], v[14:15], v[56:57], v[60:61] op_sel_hi:[1,0,1]
	v_pk_mul_f32 v[60:61], v[56:57], v[86:87] op_sel:[1,1] op_sel_hi:[0,1] neg_lo:[0,1]
	v_pk_fma_f32 v[60:61], v[56:57], v[86:87], v[60:61] op_sel_hi:[1,0,1]
	ds_write2_b64 v73, v[58:59], v[60:61] offset0:96 offset1:112
	v_pk_mul_f32 v[58:59], v[14:15], v[56:57] op_sel:[1,1] op_sel_hi:[0,1] neg_lo:[0,1]
	v_pk_fma_f32 v[56:57], v[14:15], v[56:57], v[58:59] op_sel_hi:[1,0,1]
	v_pk_mul_f32 v[58:59], v[56:57], v[46:47] op_sel:[1,1] op_sel_hi:[0,1] neg_lo:[0,1]
	v_pk_fma_f32 v[46:47], v[56:57], v[46:47], v[58:59] op_sel_hi:[1,0,1]
	v_pk_mul_f32 v[58:59], v[14:15], v[56:57] op_sel:[1,1] op_sel_hi:[0,1] neg_lo:[0,1]
	v_pk_fma_f32 v[56:57], v[14:15], v[56:57], v[58:59] op_sel_hi:[1,0,1]
	v_pk_mul_f32 v[58:59], v[56:57], v[92:93] op_sel:[1,1] op_sel_hi:[0,1] neg_lo:[0,1]
	v_pk_fma_f32 v[58:59], v[56:57], v[92:93], v[58:59] op_sel_hi:[1,0,1]
	ds_write2_b64 v72, v[46:47], v[58:59] offset0:128 offset1:144
	v_pk_mul_f32 v[46:47], v[14:15], v[56:57] op_sel:[1,1] op_sel_hi:[0,1] neg_lo:[0,1]
	v_pk_fma_f32 v[46:47], v[14:15], v[56:57], v[46:47] op_sel_hi:[1,0,1]
	v_pk_mul_f32 v[56:57], v[46:47], v[50:51] op_sel:[1,1] op_sel_hi:[0,1] neg_lo:[0,1]
	v_pk_fma_f32 v[50:51], v[46:47], v[50:51], v[56:57] op_sel_hi:[1,0,1]
	v_pk_mul_f32 v[56:57], v[14:15], v[46:47] op_sel:[1,1] op_sel_hi:[0,1] neg_lo:[0,1]
	v_pk_fma_f32 v[46:47], v[14:15], v[46:47], v[56:57] op_sel_hi:[1,0,1]
	v_pk_mul_f32 v[56:57], v[46:47], v[94:95] op_sel:[1,1] op_sel_hi:[0,1] neg_lo:[0,1]
	v_pk_fma_f32 v[56:57], v[46:47], v[94:95], v[56:57] op_sel_hi:[1,0,1]
	ds_write2_b64 v71, v[50:51], v[56:57] offset0:160 offset1:176
	v_pk_mul_f32 v[50:51], v[14:15], v[46:47] op_sel:[1,1] op_sel_hi:[0,1] neg_lo:[0,1]
	v_pk_fma_f32 v[46:47], v[14:15], v[46:47], v[50:51] op_sel_hi:[1,0,1]
	v_pk_mul_f32 v[50:51], v[38:39], v[46:47] op_sel:[1,1] op_sel_hi:[1,0] neg_lo:[1,0]
	v_pk_fma_f32 v[38:39], v[38:39], v[46:47], v[50:51] op_sel_hi:[0,1,1]
	v_pk_mul_f32 v[50:51], v[14:15], v[46:47] op_sel:[1,1] op_sel_hi:[0,1] neg_lo:[0,1]
	v_pk_fma_f32 v[46:47], v[14:15], v[46:47], v[50:51] op_sel_hi:[1,0,1]
	v_pk_mul_f32 v[50:51], v[46:47], v[78:79] op_sel:[1,1] op_sel_hi:[0,1] neg_lo:[0,1]
	v_pk_fma_f32 v[50:51], v[46:47], v[78:79], v[50:51] op_sel_hi:[1,0,1]
	ds_write2_b64 v70, v[38:39], v[50:51] offset0:192 offset1:208
	v_pk_mul_f32 v[38:39], v[14:15], v[46:47] op_sel:[1,1] op_sel_hi:[0,1] neg_lo:[0,1]
	v_pk_fma_f32 v[38:39], v[14:15], v[46:47], v[38:39] op_sel_hi:[1,0,1]
	v_pk_mul_f32 v[46:47], v[42:43], v[38:39] op_sel:[1,1] op_sel_hi:[1,0] neg_lo:[1,0]
	v_pk_fma_f32 v[42:43], v[42:43], v[38:39], v[46:47] op_sel_hi:[0,1,1]
	v_pk_mul_f32 v[46:47], v[14:15], v[38:39] op_sel:[1,1] op_sel_hi:[0,1] neg_lo:[0,1]
	v_pk_fma_f32 v[38:39], v[14:15], v[38:39], v[46:47] op_sel_hi:[1,0,1]
	v_pk_mul_f32 v[46:47], v[38:39], v[82:83] op_sel:[1,1] op_sel_hi:[0,1] neg_lo:[0,1]
	v_pk_fma_f32 v[46:47], v[38:39], v[82:83], v[46:47] op_sel_hi:[1,0,1]
	ds_write2_b64 v69, v[42:43], v[46:47] offset0:224 offset1:240
	v_pk_mul_f32 v[42:43], v[14:15], v[38:39] op_sel:[1,1] op_sel_hi:[0,1] neg_lo:[0,1]
	v_pk_fma_f32 v[38:39], v[14:15], v[38:39], v[42:43] op_sel_hi:[1,0,1]
	v_pk_mul_f32 v[42:43], v[30:31], v[38:39] op_sel:[1,1] op_sel_hi:[1,0] neg_lo:[1,0]
	v_pk_fma_f32 v[30:31], v[30:31], v[38:39], v[42:43] op_sel_hi:[0,1,1]
	v_pk_mul_f32 v[42:43], v[14:15], v[38:39] op_sel:[1,1] op_sel_hi:[0,1] neg_lo:[0,1]
	v_pk_fma_f32 v[38:39], v[14:15], v[38:39], v[42:43] op_sel_hi:[1,0,1]
	v_pk_mul_f32 v[42:43], v[80:81], v[38:39] op_sel:[1,1] op_sel_hi:[1,0] neg_lo:[1,0]
	v_pk_fma_f32 v[42:43], v[80:81], v[38:39], v[42:43] op_sel_hi:[0,1,1]
	ds_write2_b64 v68, v[30:31], v[42:43] offset1:16
	v_pk_mul_f32 v[30:31], v[14:15], v[38:39] op_sel:[1,1] op_sel_hi:[0,1] neg_lo:[0,1]
	v_pk_fma_f32 v[30:31], v[14:15], v[38:39], v[30:31] op_sel_hi:[1,0,1]
	v_pk_mul_f32 v[38:39], v[34:35], v[30:31] op_sel:[1,1] op_sel_hi:[1,0] neg_lo:[1,0]
	v_pk_fma_f32 v[34:35], v[34:35], v[30:31], v[38:39] op_sel_hi:[0,1,1]
	v_pk_mul_f32 v[38:39], v[14:15], v[30:31] op_sel:[1,1] op_sel_hi:[0,1] neg_lo:[0,1]
	v_pk_fma_f32 v[30:31], v[14:15], v[30:31], v[38:39] op_sel_hi:[1,0,1]
	v_pk_mul_f32 v[38:39], v[54:55], v[30:31] op_sel:[1,1] op_sel_hi:[1,0] neg_lo:[1,0]
	v_pk_fma_f32 v[38:39], v[54:55], v[30:31], v[38:39] op_sel_hi:[0,1,1]
	ds_write2_b64 v67, v[34:35], v[38:39] offset0:32 offset1:48
	v_pk_mul_f32 v[34:35], v[14:15], v[30:31] op_sel:[1,1] op_sel_hi:[0,1] neg_lo:[0,1]
	v_pk_fma_f32 v[30:31], v[14:15], v[30:31], v[34:35] op_sel_hi:[1,0,1]
	v_pk_mul_f32 v[34:35], v[26:27], v[30:31] op_sel:[1,1] op_sel_hi:[1,0] neg_lo:[1,0]
	v_pk_fma_f32 v[26:27], v[26:27], v[30:31], v[34:35] op_sel_hi:[0,1,1]
	v_pk_mul_f32 v[34:35], v[14:15], v[30:31] op_sel:[1,1] op_sel_hi:[0,1] neg_lo:[0,1]
	v_pk_fma_f32 v[30:31], v[14:15], v[30:31], v[34:35] op_sel_hi:[1,0,1]
	v_pk_mul_f32 v[34:35], v[48:49], v[30:31] op_sel:[1,1] op_sel_hi:[1,0] neg_lo:[1,0]
	v_pk_fma_f32 v[34:35], v[48:49], v[30:31], v[34:35] op_sel_hi:[0,1,1]
	ds_write2_b64 v66, v[26:27], v[34:35] offset0:64 offset1:80
	v_pk_mul_f32 v[26:27], v[14:15], v[30:31] op_sel:[1,1] op_sel_hi:[0,1] neg_lo:[0,1]
	v_pk_fma_f32 v[26:27], v[14:15], v[30:31], v[26:27] op_sel_hi:[1,0,1]
	v_pk_mul_f32 v[30:31], v[28:29], v[26:27] op_sel:[1,1] op_sel_hi:[1,0] neg_lo:[1,0]
	v_pk_fma_f32 v[28:29], v[28:29], v[26:27], v[30:31] op_sel_hi:[0,1,1]
	v_pk_mul_f32 v[30:31], v[14:15], v[26:27] op_sel:[1,1] op_sel_hi:[0,1] neg_lo:[0,1]
	v_pk_fma_f32 v[26:27], v[14:15], v[26:27], v[30:31] op_sel_hi:[1,0,1]
	v_pk_mul_f32 v[30:31], v[52:53], v[26:27] op_sel:[1,1] op_sel_hi:[1,0] neg_lo:[1,0]
	v_pk_fma_f32 v[30:31], v[52:53], v[26:27], v[30:31] op_sel_hi:[0,1,1]
	ds_write2_b64 v65, v[28:29], v[30:31] offset0:96 offset1:112
	v_pk_mul_f32 v[28:29], v[14:15], v[26:27] op_sel:[1,1] op_sel_hi:[0,1] neg_lo:[0,1]
	v_pk_fma_f32 v[26:27], v[14:15], v[26:27], v[28:29] op_sel_hi:[1,0,1]
	v_pk_mul_f32 v[28:29], v[22:23], v[26:27] op_sel:[1,1] op_sel_hi:[1,0] neg_lo:[1,0]
	v_pk_fma_f32 v[22:23], v[22:23], v[26:27], v[28:29] op_sel_hi:[0,1,1]
	v_pk_mul_f32 v[28:29], v[14:15], v[26:27] op_sel:[1,1] op_sel_hi:[0,1] neg_lo:[0,1]
	v_pk_fma_f32 v[26:27], v[14:15], v[26:27], v[28:29] op_sel_hi:[1,0,1]
	v_pk_mul_f32 v[28:29], v[40:41], v[26:27] op_sel:[1,1] op_sel_hi:[1,0] neg_lo:[1,0]
	v_pk_fma_f32 v[28:29], v[40:41], v[26:27], v[28:29] op_sel_hi:[0,1,1]
	ds_write2_b64 v64, v[22:23], v[28:29] offset0:128 offset1:144
	v_pk_mul_f32 v[22:23], v[14:15], v[26:27] op_sel:[1,1] op_sel_hi:[0,1] neg_lo:[0,1]
	v_pk_fma_f32 v[22:23], v[14:15], v[26:27], v[22:23] op_sel_hi:[1,0,1]
	v_pk_mul_f32 v[26:27], v[24:25], v[22:23] op_sel:[1,1] op_sel_hi:[1,0] neg_lo:[1,0]
	v_pk_fma_f32 v[24:25], v[24:25], v[22:23], v[26:27] op_sel_hi:[0,1,1]
	v_pk_mul_f32 v[26:27], v[14:15], v[22:23] op_sel:[1,1] op_sel_hi:[0,1] neg_lo:[0,1]
	v_pk_fma_f32 v[22:23], v[14:15], v[22:23], v[26:27] op_sel_hi:[1,0,1]
	v_pk_mul_f32 v[26:27], v[44:45], v[22:23] op_sel:[1,1] op_sel_hi:[1,0] neg_lo:[1,0]
	v_pk_fma_f32 v[26:27], v[44:45], v[22:23], v[26:27] op_sel_hi:[0,1,1]
	ds_write2_b64 v63, v[24:25], v[26:27] offset0:160 offset1:176
	v_pk_mul_f32 v[24:25], v[14:15], v[22:23] op_sel:[1,1] op_sel_hi:[0,1] neg_lo:[0,1]
	v_pk_fma_f32 v[22:23], v[14:15], v[22:23], v[24:25] op_sel_hi:[1,0,1]
	v_pk_mul_f32 v[24:25], v[18:19], v[22:23] op_sel:[1,1] op_sel_hi:[1,0] neg_lo:[1,0]
	v_pk_fma_f32 v[18:19], v[18:19], v[22:23], v[24:25] op_sel_hi:[0,1,1]
	v_pk_mul_f32 v[24:25], v[14:15], v[22:23] op_sel:[1,1] op_sel_hi:[0,1] neg_lo:[0,1]
	v_pk_fma_f32 v[22:23], v[14:15], v[22:23], v[24:25] op_sel_hi:[1,0,1]
	v_pk_mul_f32 v[24:25], v[32:33], v[22:23] op_sel:[1,1] op_sel_hi:[1,0] neg_lo:[1,0]
	v_pk_fma_f32 v[24:25], v[32:33], v[22:23], v[24:25] op_sel_hi:[0,1,1]
	ds_write2_b64 v62, v[18:19], v[24:25] offset0:192 offset1:208
	v_pk_mul_f32 v[18:19], v[14:15], v[22:23] op_sel:[1,1] op_sel_hi:[0,1] neg_lo:[0,1]
	v_pk_fma_f32 v[18:19], v[14:15], v[22:23], v[18:19] op_sel_hi:[1,0,1]
	v_pk_mul_f32 v[22:23], v[20:21], v[18:19] op_sel:[1,1] op_sel_hi:[1,0] neg_lo:[1,0]
	v_pk_fma_f32 v[20:21], v[20:21], v[18:19], v[22:23] op_sel_hi:[0,1,1]
	v_pk_mul_f32 v[22:23], v[14:15], v[18:19] op_sel:[1,1] op_sel_hi:[0,1] neg_lo:[0,1]
	v_pk_fma_f32 v[14:15], v[14:15], v[18:19], v[22:23] op_sel_hi:[1,0,1]
	v_pk_mul_f32 v[18:19], v[36:37], v[14:15] op_sel:[1,1] op_sel_hi:[1,0] neg_lo:[1,0]
	v_pk_fma_f32 v[14:15], v[36:37], v[14:15], v[18:19] op_sel_hi:[0,1,1]
	ds_write2_b64 v13, v[20:21], v[14:15] offset0:224 offset1:240
	v_mov_b32_e32 v14, v182
	v_mov_b32_e32 v10, v176
	v_mov_b32_e32 v13, v175
	s_waitcnt lgkmcnt(0)
	s_barrier
	v_mov_b32_e32 v50, v167
	v_xor_b32_e32 v18, 1, v13
	v_lshlrev_b32_e32 v10, 3, v10
	v_lshlrev_b32_e32 v18, 3, v18
	v_add3_u32 v20, 0, v18, v10
	v_xor_b32_e32 v18, 2, v13
	v_lshlrev_b32_e32 v18, 3, v18
	v_xor_b32_e32 v26, 5, v13
	v_add3_u32 v22, 0, v18, v10
	v_xor_b32_e32 v18, 3, v13
	v_lshlrev_b32_e32 v26, 3, v26
	v_lshlrev_b32_e32 v15, 3, v13
	v_lshlrev_b32_e32 v18, 3, v18
	v_add3_u32 v28, 0, v26, v10
	v_xor_b32_e32 v26, 6, v13
	v_add3_u32 v15, 0, v15, v10
	v_add3_u32 v24, 0, v18, v10
	v_lshlrev_b32_e32 v26, 3, v26
	v_xor_b32_e32 v34, 9, v13
	ds_read_b64 v[18:19], v15
	ds_read_b64 v[20:21], v20
	ds_read_b64 v[22:23], v22
	ds_read_b64 v[24:25], v24
	v_xor_b32_e32 v15, 4, v13
	v_add3_u32 v30, 0, v26, v10
	v_xor_b32_e32 v26, 7, v13
	v_lshlrev_b32_e32 v34, 3, v34
	v_lshlrev_b32_e32 v15, 3, v15
	v_lshlrev_b32_e32 v26, 3, v26
	v_add3_u32 v36, 0, v34, v10
	v_xor_b32_e32 v34, 10, v13
	v_add3_u32 v15, 0, v15, v10
	v_add3_u32 v32, 0, v26, v10
	v_lshlrev_b32_e32 v34, 3, v34
	ds_read_b64 v[26:27], v15
	ds_read_b64 v[28:29], v28
	ds_read_b64 v[30:31], v30
	ds_read_b64 v[32:33], v32
	v_xor_b32_e32 v15, 8, v13
	v_add3_u32 v38, 0, v34, v10
	v_xor_b32_e32 v34, 11, v13
	v_lshlrev_b32_e32 v15, 3, v15
	v_lshlrev_b32_e32 v34, 3, v34
	v_xor_b32_e32 v42, 13, v13
	v_add3_u32 v15, 0, v15, v10
	v_add3_u32 v40, 0, v34, v10
	v_lshlrev_b32_e32 v42, 3, v42
	ds_read_b64 v[34:35], v15
	ds_read_b64 v[36:37], v36
	ds_read_b64 v[38:39], v38
	ds_read_b64 v[40:41], v40
	v_xor_b32_e32 v15, 12, v13
	v_add3_u32 v44, 0, v42, v10
	v_xor_b32_e32 v42, 14, v13
	v_xor_b32_e32 v13, 15, v13
	v_lshlrev_b32_e32 v15, 3, v15
	v_lshlrev_b32_e32 v42, 3, v42
	v_lshlrev_b32_e32 v13, 3, v13
	v_add3_u32 v15, 0, v15, v10
	v_add3_u32 v46, 0, v42, v10
	v_add3_u32 v10, 0, v13, v10
	ds_read_b64 v[42:43], v15
	ds_read_b64 v[44:45], v44
	ds_read_b64 v[46:47], v46
	ds_read_b64 v[48:49], v10
	v_mov_b32_e32 v10, v1
	v_mov_b32_e32 v13, v166
	v_mov_b32_e32 v10, v164
	s_waitcnt lgkmcnt(7)
	v_pk_add_f32 v[54:55], v[18:19], v[34:35]
	v_mov_b32_e32 v10, v165
	v_pk_add_f32 v[18:19], v[18:19], v[34:35] neg_lo:[0,1] neg_hi:[0,1]
	s_waitcnt lgkmcnt(6)
	v_pk_add_f32 v[34:35], v[20:21], v[36:37]
	v_pk_add_f32 v[20:21], v[20:21], v[36:37] neg_lo:[0,1] neg_hi:[0,1]
	v_mov_b32_e32 v13, v168
	v_mov_b32_e32 v52, v169
	v_ashrrev_i32_e32 v15, 31, v14
	v_pk_mul_f32 v[36:37], v[20:21], v[52:53] op_sel:[1,0] op_sel_hi:[0,0] neg_lo:[1,1] neg_hi:[0,1]
	v_mov_b32_e32 v13, v170
	v_pk_fma_f32 v[20:21], v[20:21], v[10:11], v[36:37] op_sel_hi:[1,0,1]
	s_waitcnt lgkmcnt(5)
	v_pk_add_f32 v[36:37], v[22:23], v[38:39]
	v_pk_add_f32 v[22:23], v[22:23], v[38:39] neg_lo:[0,1] neg_hi:[0,1]
	s_movk_i32 s0, 0x1000
	v_pk_mul_f32 v[38:39], v[22:23], v[50:51] op_sel:[1,0] op_sel_hi:[0,0] neg_lo:[1,1] neg_hi:[0,1]
	v_mov_b32_e32 v13, v171
	v_pk_fma_f32 v[22:23], v[22:23], v[50:51], v[38:39] op_sel_hi:[1,0,1]
	s_waitcnt lgkmcnt(4)
	v_pk_add_f32 v[38:39], v[24:25], v[40:41]
	v_pk_add_f32 v[24:25], v[24:25], v[40:41] neg_lo:[0,1] neg_hi:[0,1]
	v_mov_b32_e32 v72, v164
	v_pk_mul_f32 v[40:41], v[24:25], v[52:53] op_sel_hi:[1,0]
	v_pk_fma_f32 v[24:25], v[24:25], v[10:11], v[40:41] op_sel:[1,0,0] op_sel_hi:[0,0,1] neg_lo:[1,1,0] neg_hi:[0,1,0]
	s_waitcnt lgkmcnt(3)
	v_pk_add_f32 v[40:41], v[26:27], v[42:43]
	v_pk_add_f32 v[26:27], v[26:27], v[42:43] neg_lo:[0,1] neg_hi:[0,1]
	v_mov_b32_e32 v13, v175
	v_xor_b32_e32 v43, 0x80000000, v26
	v_mov_b32_e32 v42, v27
	s_waitcnt lgkmcnt(2)
	v_pk_add_f32 v[26:27], v[28:29], v[44:45]
	v_pk_add_f32 v[28:29], v[28:29], v[44:45] neg_lo:[0,1] neg_hi:[0,1]
	v_mov_b32_e32 v74, v166
	v_pk_mul_f32 v[44:45], v[28:29], v[52:53] op_sel_hi:[1,0] neg_lo:[0,1] neg_hi:[0,1]
	v_pk_fma_f32 v[28:29], v[28:29], v[10:11], v[44:45] op_sel:[1,0,0] op_sel_hi:[0,0,1] neg_lo:[1,1,0] neg_hi:[0,1,0]
	s_waitcnt lgkmcnt(1)
	v_pk_add_f32 v[44:45], v[30:31], v[46:47]
	v_pk_add_f32 v[30:31], v[30:31], v[46:47] neg_lo:[0,1] neg_hi:[0,1]
	v_mov_b32_e32 v76, v168
	v_pk_mul_f32 v[46:47], v[30:31], v[50:51] op_sel:[1,0] op_sel_hi:[0,0] neg_lo:[1,1] neg_hi:[0,1]
	v_mov_b32_e32 v78, v170
	v_pk_fma_f32 v[30:31], v[30:31], v[50:51], v[46:47] op_sel_hi:[1,0,1] neg_lo:[0,1,0] neg_hi:[0,1,0]
	s_waitcnt lgkmcnt(0)
	v_pk_add_f32 v[46:47], v[32:33], v[48:49]
	v_pk_add_f32 v[32:33], v[32:33], v[48:49] neg_lo:[0,1] neg_hi:[0,1]
	v_mov_b32_e32 v83, v11
	v_pk_mul_f32 v[48:49], v[32:33], v[52:53] op_sel:[1,0] op_sel_hi:[0,0] neg_lo:[1,1] neg_hi:[0,1]
	v_pk_add_f32 v[52:53], v[34:35], v[26:27]
	v_pk_add_f32 v[26:27], v[34:35], v[26:27] neg_lo:[0,1] neg_hi:[0,1]
	v_pk_fma_f32 v[32:33], v[32:33], v[10:11], v[48:49] op_sel_hi:[1,0,1] neg_lo:[0,1,0] neg_hi:[0,1,0]
	v_pk_mul_f32 v[34:35], v[26:27], v[50:51] op_sel:[1,0] op_sel_hi:[0,0] neg_lo:[1,1] neg_hi:[0,1]
	v_pk_add_f32 v[48:49], v[54:55], v[40:41]
	v_pk_fma_f32 v[26:27], v[26:27], v[50:51], v[34:35] op_sel_hi:[1,0,1]
	v_pk_add_f32 v[34:35], v[36:37], v[44:45]
	v_pk_add_f32 v[36:37], v[36:37], v[44:45] neg_lo:[0,1] neg_hi:[0,1]
	v_pk_add_f32 v[40:41], v[54:55], v[40:41] neg_lo:[0,1] neg_hi:[0,1]
	v_xor_b32_e32 v45, 0x80000000, v36
	v_mov_b32_e32 v44, v37
	v_pk_add_f32 v[36:37], v[38:39], v[46:47]
	v_pk_add_f32 v[38:39], v[38:39], v[46:47] neg_lo:[0,1] neg_hi:[0,1]
	v_mov_b32_e32 v10, v177
	v_pk_mul_f32 v[46:47], v[38:39], v[50:51] op_sel:[1,0] op_sel_hi:[0,0] neg_lo:[1,1] neg_hi:[0,1]
	s_mov_b32 s7, 0xa000
	v_pk_fma_f32 v[38:39], v[38:39], v[50:51], v[46:47] op_sel_hi:[1,0,1] neg_lo:[0,1,0] neg_hi:[0,1,0]
	v_pk_add_f32 v[46:47], v[48:49], v[34:35]
	v_pk_add_f32 v[34:35], v[48:49], v[34:35] neg_lo:[0,1] neg_hi:[0,1]
	v_pk_add_f32 v[48:49], v[52:53], v[36:37]
	v_pk_add_f32 v[36:37], v[52:53], v[36:37] neg_lo:[0,1] neg_hi:[0,1]
	s_mov_b32 s6, 0xc000
	v_xor_b32_e32 v53, 0x80000000, v36
	v_mov_b32_e32 v52, v37
	v_pk_add_f32 v[36:37], v[46:47], v[48:49]
	v_pk_add_f32 v[46:47], v[46:47], v[48:49] neg_lo:[0,1] neg_hi:[0,1]
	v_pk_add_f32 v[48:49], v[34:35], v[52:53]
	v_pk_add_f32 v[34:35], v[34:35], v[52:53] neg_lo:[0,1] neg_hi:[0,1]
	v_pk_add_f32 v[52:53], v[40:41], v[44:45]
	v_pk_add_f32 v[40:41], v[40:41], v[44:45] neg_lo:[0,1] neg_hi:[0,1]
	v_pk_add_f32 v[44:45], v[26:27], v[38:39]
	v_pk_add_f32 v[26:27], v[26:27], v[38:39] neg_lo:[0,1] neg_hi:[0,1]
	s_mov_b32 s1, 0xe000
	v_xor_b32_e32 v39, 0x80000000, v26
	v_mov_b32_e32 v38, v27
	v_pk_add_f32 v[26:27], v[52:53], v[44:45]
	v_pk_add_f32 v[44:45], v[52:53], v[44:45] neg_lo:[0,1] neg_hi:[0,1]
	v_pk_add_f32 v[52:53], v[40:41], v[38:39]
	v_pk_add_f32 v[38:39], v[40:41], v[38:39] neg_lo:[0,1] neg_hi:[0,1]
	v_pk_add_f32 v[40:41], v[18:19], v[42:43]
	v_pk_add_f32 v[18:19], v[18:19], v[42:43] neg_lo:[0,1] neg_hi:[0,1]
	v_pk_add_f32 v[42:43], v[20:21], v[28:29]
	v_pk_add_f32 v[20:21], v[20:21], v[28:29] neg_lo:[0,1] neg_hi:[0,1]
	s_mov_b32 s8, 0x8000
	v_pk_mul_f32 v[28:29], v[50:51], v[20:21] op_sel:[0,1] op_sel_hi:[0,0] neg_lo:[1,1] neg_hi:[1,0]
	v_pk_fma_f32 v[20:21], v[50:51], v[20:21], v[28:29] op_sel_hi:[0,1,1]
	v_pk_add_f32 v[28:29], v[22:23], v[30:31]
	v_pk_add_f32 v[22:23], v[22:23], v[30:31] neg_lo:[0,1] neg_hi:[0,1]
	s_mov_b32 s9, 0x9000
	v_xor_b32_e32 v31, 0x80000000, v22
	v_mov_b32_e32 v30, v23
	v_pk_add_f32 v[22:23], v[24:25], v[32:33]
	v_pk_add_f32 v[24:25], v[24:25], v[32:33] neg_lo:[0,1] neg_hi:[0,1]
	s_mov_b32 s5, 0xb000
	v_pk_mul_f32 v[32:33], v[50:51], v[24:25] op_sel:[0,1] op_sel_hi:[0,0] neg_lo:[1,1] neg_hi:[1,0]
	v_pk_fma_f32 v[24:25], v[50:51], v[24:25], v[32:33] op_sel_hi:[0,1,1] neg_lo:[1,0,0] neg_hi:[1,0,0]
	v_pk_add_f32 v[32:33], v[40:41], v[28:29]
	v_pk_add_f32 v[28:29], v[40:41], v[28:29] neg_lo:[0,1] neg_hi:[0,1]
	v_pk_add_f32 v[40:41], v[42:43], v[22:23]
	v_pk_add_f32 v[22:23], v[42:43], v[22:23] neg_lo:[0,1] neg_hi:[0,1]
	v_mov_b32_e32 v50, v167
	v_xor_b32_e32 v43, 0x80000000, v22
	v_mov_b32_e32 v42, v23
	v_pk_add_f32 v[22:23], v[32:33], v[40:41]
	v_pk_add_f32 v[32:33], v[32:33], v[40:41] neg_lo:[0,1] neg_hi:[0,1]
	v_pk_add_f32 v[40:41], v[28:29], v[42:43]
	v_pk_add_f32 v[28:29], v[28:29], v[42:43] neg_lo:[0,1] neg_hi:[0,1]
	v_pk_add_f32 v[42:43], v[18:19], v[30:31]
	v_pk_add_f32 v[18:19], v[18:19], v[30:31] neg_lo:[0,1] neg_hi:[0,1]
	v_pk_add_f32 v[30:31], v[20:21], v[24:25]
	v_pk_add_f32 v[20:21], v[20:21], v[24:25] neg_lo:[0,1] neg_hi:[0,1]
	s_mov_b32 s4, 0xd000
	v_xor_b32_e32 v25, 0x80000000, v20
	v_mov_b32_e32 v24, v21
	v_pk_add_f32 v[20:21], v[42:43], v[30:31]
	v_pk_add_f32 v[30:31], v[42:43], v[30:31] neg_lo:[0,1] neg_hi:[0,1]
	v_pk_add_f32 v[42:43], v[18:19], v[24:25]
	v_pk_add_f32 v[18:19], v[18:19], v[24:25] neg_lo:[0,1] neg_hi:[0,1]
	v_lshl_add_u64 v[24:25], v[14:15], 3, s[46:47]
	global_store_dwordx2 v[24:25], v[36:37], off
	v_add_u32_e32 v24, 0x200, v14
	v_ashrrev_i32_e32 v25, 31, v24
	v_lshl_add_u64 v[24:25], v[24:25], 3, s[46:47]
	global_store_dwordx2 v[24:25], v[22:23], off
	v_add_u32_e32 v22, 0x400, v14
	v_ashrrev_i32_e32 v23, 31, v22
	v_lshl_add_u64 v[22:23], v[22:23], 3, s[46:47]
	global_store_dwordx2 v[22:23], v[26:27], off
	v_add_u32_e32 v22, 0x600, v14
	v_ashrrev_i32_e32 v23, 31, v22
	v_lshl_add_u64 v[22:23], v[22:23], 3, s[46:47]
	global_store_dwordx2 v[22:23], v[20:21], off
	v_add_u32_e32 v20, 0x800, v14
	v_ashrrev_i32_e32 v21, 31, v20
	v_lshl_add_u64 v[20:21], v[20:21], 3, s[46:47]
	global_store_dwordx2 v[20:21], v[48:49], off
	v_add_u32_e32 v20, 0xa00, v14
	v_ashrrev_i32_e32 v21, 31, v20
	v_lshl_add_u64 v[20:21], v[20:21], 3, s[46:47]
	global_store_dwordx2 v[20:21], v[40:41], off
	v_add_u32_e32 v20, 0xc00, v14
	v_ashrrev_i32_e32 v21, 31, v20
	v_lshl_add_u64 v[20:21], v[20:21], 3, s[46:47]
	global_store_dwordx2 v[20:21], v[52:53], off
	v_add_u32_e32 v20, 0xe00, v14
	v_ashrrev_i32_e32 v21, 31, v20
	v_lshl_add_u64 v[20:21], v[20:21], 3, s[46:47]
	global_store_dwordx2 v[20:21], v[42:43], off
	v_add_u32_e32 v20, 0x1000, v14
	v_ashrrev_i32_e32 v21, 31, v20
	v_lshl_add_u64 v[20:21], v[20:21], 3, s[46:47]
	global_store_dwordx2 v[20:21], v[46:47], off
	v_add_u32_e32 v20, 0x1200, v14
	v_ashrrev_i32_e32 v21, 31, v20
	v_lshl_add_u64 v[20:21], v[20:21], 3, s[46:47]
	global_store_dwordx2 v[20:21], v[32:33], off
	v_add_u32_e32 v20, 0x1400, v14
	v_ashrrev_i32_e32 v21, 31, v20
	v_lshl_add_u64 v[20:21], v[20:21], 3, s[46:47]
	global_store_dwordx2 v[20:21], v[44:45], off
	v_add_u32_e32 v20, 0x1600, v14
	v_ashrrev_i32_e32 v21, 31, v20
	v_lshl_add_u64 v[20:21], v[20:21], 3, s[46:47]
	global_store_dwordx2 v[20:21], v[30:31], off
	v_add_u32_e32 v20, 0x1800, v14
	v_ashrrev_i32_e32 v21, 31, v20
	v_lshl_add_u64 v[20:21], v[20:21], 3, s[46:47]
	global_store_dwordx2 v[20:21], v[34:35], off
	v_add_u32_e32 v20, 0x1a00, v14
	v_ashrrev_i32_e32 v21, 31, v20
	v_lshl_add_u64 v[20:21], v[20:21], 3, s[46:47]
	global_store_dwordx2 v[20:21], v[28:29], off
	v_add_u32_e32 v20, 0x1c00, v14
	v_ashrrev_i32_e32 v21, 31, v20
	v_lshl_add_u64 v[20:21], v[20:21], 3, s[46:47]
	global_store_dwordx2 v[20:21], v[38:39], off
	v_add_u32_e32 v20, 0x1e00, v14
	v_ashrrev_i32_e32 v21, 31, v20
	v_lshl_add_u64 v[20:21], v[20:21], 3, s[46:47]
	global_store_dwordx2 v[20:21], v[18:19], off
	v_mov_b32_e32 v52, v169
	v_xor_b32_e32 v18, 1, v13
	v_lshlrev_b32_e32 v10, 3, v10
	v_lshlrev_b32_e32 v18, 3, v18
	v_add3_u32 v20, 0, v18, v10
	v_xor_b32_e32 v18, 2, v13
	v_lshlrev_b32_e32 v18, 3, v18
	v_xor_b32_e32 v26, 5, v13
	v_add3_u32 v22, 0, v18, v10
	v_xor_b32_e32 v18, 3, v13
	v_lshlrev_b32_e32 v26, 3, v26
	v_lshlrev_b32_e32 v15, 3, v13
	v_lshlrev_b32_e32 v18, 3, v18
	v_add3_u32 v28, 0, v26, v10
	v_xor_b32_e32 v26, 6, v13
	v_add3_u32 v15, 0, v15, v10
	v_add3_u32 v24, 0, v18, v10
	v_lshlrev_b32_e32 v26, 3, v26
	v_xor_b32_e32 v34, 9, v13
	ds_read_b64 v[18:19], v15
	ds_read_b64 v[20:21], v20
	ds_read_b64 v[22:23], v22
	ds_read_b64 v[24:25], v24
	v_xor_b32_e32 v15, 4, v13
	v_add3_u32 v30, 0, v26, v10
	v_xor_b32_e32 v26, 7, v13
	v_lshlrev_b32_e32 v34, 3, v34
	v_lshlrev_b32_e32 v15, 3, v15
	v_lshlrev_b32_e32 v26, 3, v26
	v_add3_u32 v36, 0, v34, v10
	v_xor_b32_e32 v34, 10, v13
	v_add3_u32 v15, 0, v15, v10
	v_add3_u32 v32, 0, v26, v10
	v_lshlrev_b32_e32 v34, 3, v34
	ds_read_b64 v[26:27], v15
	ds_read_b64 v[28:29], v28
	ds_read_b64 v[30:31], v30
	ds_read_b64 v[32:33], v32
	v_xor_b32_e32 v15, 8, v13
	v_add3_u32 v38, 0, v34, v10
	v_xor_b32_e32 v34, 11, v13
	v_lshlrev_b32_e32 v15, 3, v15
	v_lshlrev_b32_e32 v34, 3, v34
	v_xor_b32_e32 v42, 13, v13
	v_add3_u32 v15, 0, v15, v10
	v_add3_u32 v40, 0, v34, v10
	v_lshlrev_b32_e32 v42, 3, v42
	ds_read_b64 v[34:35], v15
	ds_read_b64 v[36:37], v36
	ds_read_b64 v[38:39], v38
	ds_read_b64 v[40:41], v40
	v_xor_b32_e32 v15, 12, v13
	v_add3_u32 v44, 0, v42, v10
	v_xor_b32_e32 v42, 14, v13
	v_xor_b32_e32 v13, 15, v13
	v_lshlrev_b32_e32 v15, 3, v15
	v_lshlrev_b32_e32 v42, 3, v42
	v_lshlrev_b32_e32 v13, 3, v13
	v_add3_u32 v15, 0, v15, v10
	v_add3_u32 v46, 0, v42, v10
	v_add3_u32 v10, 0, v13, v10
	ds_read_b64 v[42:43], v15
	ds_read_b64 v[44:45], v44
	ds_read_b64 v[46:47], v46
	ds_read_b64 v[48:49], v10
	v_mov_b32_e32 v10, v1
	v_mov_b32_e32 v13, v166
	v_mov_b32_e32 v10, v164
	s_waitcnt lgkmcnt(7)
	v_pk_add_f32 v[54:55], v[18:19], v[34:35]
	v_mov_b32_e32 v10, v165
	v_pk_add_f32 v[18:19], v[18:19], v[34:35] neg_lo:[0,1] neg_hi:[0,1]
	s_waitcnt lgkmcnt(6)
	v_pk_add_f32 v[34:35], v[20:21], v[36:37]
	v_pk_add_f32 v[20:21], v[20:21], v[36:37] neg_lo:[0,1] neg_hi:[0,1]
	v_mov_b32_e32 v13, v168
	s_nop 0
	v_pk_mul_f32 v[36:37], v[20:21], v[52:53] op_sel:[1,0] op_sel_hi:[0,0] neg_lo:[1,1] neg_hi:[0,1]
	v_mov_b32_e32 v13, v170
	v_pk_fma_f32 v[20:21], v[20:21], v[10:11], v[36:37] op_sel_hi:[1,0,1]
	s_waitcnt lgkmcnt(5)
	v_pk_add_f32 v[36:37], v[22:23], v[38:39]
	v_pk_add_f32 v[22:23], v[22:23], v[38:39] neg_lo:[0,1] neg_hi:[0,1]
	v_pk_mul_f32 v[38:39], v[22:23], v[50:51] op_sel:[1,0] op_sel_hi:[0,0] neg_lo:[1,1] neg_hi:[0,1]
	v_mov_b32_e32 v13, v171
	v_pk_fma_f32 v[22:23], v[22:23], v[50:51], v[38:39] op_sel_hi:[1,0,1]
	s_waitcnt lgkmcnt(4)
	v_pk_add_f32 v[38:39], v[24:25], v[40:41]
	v_pk_add_f32 v[24:25], v[24:25], v[40:41] neg_lo:[0,1] neg_hi:[0,1]
	v_pk_mul_f32 v[40:41], v[24:25], v[52:53] op_sel_hi:[1,0]
	v_pk_fma_f32 v[24:25], v[24:25], v[10:11], v[40:41] op_sel:[1,0,0] op_sel_hi:[0,0,1] neg_lo:[1,1,0] neg_hi:[0,1,0]
	s_waitcnt lgkmcnt(3)
	v_pk_add_f32 v[40:41], v[26:27], v[42:43]
	v_pk_add_f32 v[26:27], v[26:27], v[42:43] neg_lo:[0,1] neg_hi:[0,1]
	v_xor_b32_e32 v43, 0x80000000, v26
	v_mov_b32_e32 v42, v27
	s_waitcnt lgkmcnt(2)
	v_pk_add_f32 v[26:27], v[28:29], v[44:45]
	v_pk_add_f32 v[28:29], v[28:29], v[44:45] neg_lo:[0,1] neg_hi:[0,1]
	v_pk_mul_f32 v[44:45], v[28:29], v[52:53] op_sel_hi:[1,0] neg_lo:[0,1] neg_hi:[0,1]
	v_pk_fma_f32 v[28:29], v[28:29], v[10:11], v[44:45] op_sel:[1,0,0] op_sel_hi:[0,0,1] neg_lo:[1,1,0] neg_hi:[0,1,0]
	s_waitcnt lgkmcnt(1)
	v_pk_add_f32 v[44:45], v[30:31], v[46:47]
	v_pk_add_f32 v[30:31], v[30:31], v[46:47] neg_lo:[0,1] neg_hi:[0,1]
	v_pk_mul_f32 v[46:47], v[30:31], v[50:51] op_sel:[1,0] op_sel_hi:[0,0] neg_lo:[1,1] neg_hi:[0,1]
	v_pk_fma_f32 v[30:31], v[30:31], v[50:51], v[46:47] op_sel_hi:[1,0,1] neg_lo:[0,1,0] neg_hi:[0,1,0]
	s_waitcnt lgkmcnt(0)
	v_pk_add_f32 v[46:47], v[32:33], v[48:49]
	v_pk_add_f32 v[32:33], v[32:33], v[48:49] neg_lo:[0,1] neg_hi:[0,1]
	v_pk_mul_f32 v[48:49], v[32:33], v[52:53] op_sel:[1,0] op_sel_hi:[0,0] neg_lo:[1,1] neg_hi:[0,1]
	v_pk_add_f32 v[52:53], v[34:35], v[26:27]
	v_pk_add_f32 v[26:27], v[34:35], v[26:27] neg_lo:[0,1] neg_hi:[0,1]
	v_pk_fma_f32 v[32:33], v[32:33], v[10:11], v[48:49] op_sel_hi:[1,0,1] neg_lo:[0,1,0] neg_hi:[0,1,0]
	v_pk_mul_f32 v[34:35], v[26:27], v[50:51] op_sel:[1,0] op_sel_hi:[0,0] neg_lo:[1,1] neg_hi:[0,1]
	v_pk_add_f32 v[48:49], v[54:55], v[40:41]
	v_pk_fma_f32 v[26:27], v[26:27], v[50:51], v[34:35] op_sel_hi:[1,0,1]
	v_pk_add_f32 v[34:35], v[36:37], v[44:45]
	v_pk_add_f32 v[36:37], v[36:37], v[44:45] neg_lo:[0,1] neg_hi:[0,1]
	v_pk_add_f32 v[40:41], v[54:55], v[40:41] neg_lo:[0,1] neg_hi:[0,1]
	v_xor_b32_e32 v45, 0x80000000, v36
	v_mov_b32_e32 v44, v37
	v_pk_add_f32 v[36:37], v[38:39], v[46:47]
	v_pk_add_f32 v[38:39], v[38:39], v[46:47] neg_lo:[0,1] neg_hi:[0,1]
	v_mov_b32_e32 v10, v1
	v_pk_mul_f32 v[46:47], v[38:39], v[50:51] op_sel:[1,0] op_sel_hi:[0,0] neg_lo:[1,1] neg_hi:[0,1]
	v_pk_fma_f32 v[38:39], v[38:39], v[50:51], v[46:47] op_sel_hi:[1,0,1] neg_lo:[0,1,0] neg_hi:[0,1,0]
	v_pk_add_f32 v[46:47], v[48:49], v[34:35]
	v_pk_add_f32 v[34:35], v[48:49], v[34:35] neg_lo:[0,1] neg_hi:[0,1]
	v_pk_add_f32 v[48:49], v[52:53], v[36:37]
	v_pk_add_f32 v[36:37], v[52:53], v[36:37] neg_lo:[0,1] neg_hi:[0,1]
	v_xor_b32_e32 v53, 0x80000000, v36
	v_mov_b32_e32 v52, v37
	v_pk_add_f32 v[36:37], v[46:47], v[48:49]
	v_pk_add_f32 v[46:47], v[46:47], v[48:49] neg_lo:[0,1] neg_hi:[0,1]
	v_pk_add_f32 v[48:49], v[34:35], v[52:53]
	v_pk_add_f32 v[34:35], v[34:35], v[52:53] neg_lo:[0,1] neg_hi:[0,1]
	v_pk_add_f32 v[52:53], v[40:41], v[44:45]
	v_pk_add_f32 v[40:41], v[40:41], v[44:45] neg_lo:[0,1] neg_hi:[0,1]
	v_pk_add_f32 v[44:45], v[26:27], v[38:39]
	v_pk_add_f32 v[26:27], v[26:27], v[38:39] neg_lo:[0,1] neg_hi:[0,1]
	v_xor_b32_e32 v39, 0x80000000, v26
	v_mov_b32_e32 v38, v27
	v_pk_add_f32 v[26:27], v[52:53], v[44:45]
	v_pk_add_f32 v[44:45], v[52:53], v[44:45] neg_lo:[0,1] neg_hi:[0,1]
	v_pk_add_f32 v[52:53], v[40:41], v[38:39]
	v_pk_add_f32 v[38:39], v[40:41], v[38:39] neg_lo:[0,1] neg_hi:[0,1]
	v_pk_add_f32 v[40:41], v[18:19], v[42:43]
	v_pk_add_f32 v[18:19], v[18:19], v[42:43] neg_lo:[0,1] neg_hi:[0,1]
	v_pk_add_f32 v[42:43], v[20:21], v[28:29]
	v_pk_add_f32 v[20:21], v[20:21], v[28:29] neg_lo:[0,1] neg_hi:[0,1]
	v_pk_mul_f32 v[28:29], v[50:51], v[20:21] op_sel:[0,1] op_sel_hi:[0,0] neg_lo:[1,1] neg_hi:[1,0]
	v_pk_fma_f32 v[20:21], v[50:51], v[20:21], v[28:29] op_sel_hi:[0,1,1]
	v_pk_add_f32 v[28:29], v[22:23], v[30:31]
	v_pk_add_f32 v[22:23], v[22:23], v[30:31] neg_lo:[0,1] neg_hi:[0,1]
	v_xor_b32_e32 v31, 0x80000000, v22
	v_mov_b32_e32 v30, v23
	v_pk_add_f32 v[22:23], v[24:25], v[32:33]
	v_pk_add_f32 v[24:25], v[24:25], v[32:33] neg_lo:[0,1] neg_hi:[0,1]
	v_pk_mul_f32 v[32:33], v[50:51], v[24:25] op_sel:[0,1] op_sel_hi:[0,0] neg_lo:[1,1] neg_hi:[1,0]
	v_pk_fma_f32 v[24:25], v[50:51], v[24:25], v[32:33] op_sel_hi:[0,1,1] neg_lo:[1,0,0] neg_hi:[1,0,0]
	v_pk_add_f32 v[32:33], v[40:41], v[28:29]
	v_pk_add_f32 v[28:29], v[40:41], v[28:29] neg_lo:[0,1] neg_hi:[0,1]
	v_pk_add_f32 v[40:41], v[42:43], v[22:23]
	v_pk_add_f32 v[22:23], v[42:43], v[22:23] neg_lo:[0,1] neg_hi:[0,1]
	v_xor_b32_e32 v43, 0x80000000, v22
	v_mov_b32_e32 v42, v23
	v_pk_add_f32 v[22:23], v[32:33], v[40:41]
	v_pk_add_f32 v[32:33], v[32:33], v[40:41] neg_lo:[0,1] neg_hi:[0,1]
	v_pk_add_f32 v[40:41], v[28:29], v[42:43]
	v_pk_add_f32 v[28:29], v[28:29], v[42:43] neg_lo:[0,1] neg_hi:[0,1]
	v_pk_add_f32 v[42:43], v[18:19], v[30:31]
	v_pk_add_f32 v[18:19], v[18:19], v[30:31] neg_lo:[0,1] neg_hi:[0,1]
	v_pk_add_f32 v[30:31], v[20:21], v[24:25]
	v_pk_add_f32 v[20:21], v[20:21], v[24:25] neg_lo:[0,1] neg_hi:[0,1]
	v_xor_b32_e32 v25, 0x80000000, v20
	v_mov_b32_e32 v24, v21
	v_pk_add_f32 v[20:21], v[42:43], v[30:31]
	v_pk_add_f32 v[30:31], v[42:43], v[30:31] neg_lo:[0,1] neg_hi:[0,1]
	v_pk_add_f32 v[42:43], v[18:19], v[24:25]
	v_pk_add_f32 v[18:19], v[18:19], v[24:25] neg_lo:[0,1] neg_hi:[0,1]
	v_add_u32_e32 v24, 0x2000, v14
	v_ashrrev_i32_e32 v25, 31, v24
	v_lshl_add_u64 v[24:25], v[24:25], 3, s[46:47]
	global_store_dwordx2 v[24:25], v[36:37], off
	v_add_u32_e32 v24, 0x2200, v14
	v_ashrrev_i32_e32 v25, 31, v24
	v_lshl_add_u64 v[24:25], v[24:25], 3, s[46:47]
	global_store_dwordx2 v[24:25], v[22:23], off
	v_add_u32_e32 v22, 0x2400, v14
	v_ashrrev_i32_e32 v23, 31, v22
	v_lshl_add_u64 v[22:23], v[22:23], 3, s[46:47]
	global_store_dwordx2 v[22:23], v[26:27], off
	v_add_u32_e32 v22, 0x2600, v14
	v_ashrrev_i32_e32 v23, 31, v22
	v_lshl_add_u64 v[22:23], v[22:23], 3, s[46:47]
	global_store_dwordx2 v[22:23], v[20:21], off
	v_add_u32_e32 v20, 0x2800, v14
	v_ashrrev_i32_e32 v21, 31, v20
	v_lshl_add_u64 v[20:21], v[20:21], 3, s[46:47]
	global_store_dwordx2 v[20:21], v[48:49], off
	v_add_u32_e32 v20, 0x2a00, v14
	v_ashrrev_i32_e32 v21, 31, v20
	v_lshl_add_u64 v[20:21], v[20:21], 3, s[46:47]
	global_store_dwordx2 v[20:21], v[40:41], off
	v_add_u32_e32 v20, 0x2c00, v14
	v_ashrrev_i32_e32 v21, 31, v20
	v_lshl_add_u64 v[20:21], v[20:21], 3, s[46:47]
	global_store_dwordx2 v[20:21], v[52:53], off
	v_add_u32_e32 v20, 0x2e00, v14
	v_ashrrev_i32_e32 v21, 31, v20
	v_lshl_add_u64 v[20:21], v[20:21], 3, s[46:47]
	global_store_dwordx2 v[20:21], v[42:43], off
	v_add_u32_e32 v20, 0x3000, v14
	v_ashrrev_i32_e32 v21, 31, v20
	v_lshl_add_u64 v[20:21], v[20:21], 3, s[46:47]
	global_store_dwordx2 v[20:21], v[46:47], off
	v_add_u32_e32 v20, 0x3200, v14
	v_ashrrev_i32_e32 v21, 31, v20
	v_lshl_add_u64 v[20:21], v[20:21], 3, s[46:47]
	global_store_dwordx2 v[20:21], v[32:33], off
	v_add_u32_e32 v20, 0x3400, v14
	v_ashrrev_i32_e32 v21, 31, v20
	v_lshl_add_u64 v[20:21], v[20:21], 3, s[46:47]
	global_store_dwordx2 v[20:21], v[44:45], off
	v_add_u32_e32 v20, 0x3600, v14
	v_ashrrev_i32_e32 v21, 31, v20
	v_lshl_add_u64 v[20:21], v[20:21], 3, s[46:47]
	global_store_dwordx2 v[20:21], v[30:31], off
	v_add_u32_e32 v20, 0x3800, v14
	v_ashrrev_i32_e32 v21, 31, v20
	v_lshl_add_u64 v[20:21], v[20:21], 3, s[46:47]
	global_store_dwordx2 v[20:21], v[34:35], off
	v_add_u32_e32 v20, 0x3a00, v14
	v_ashrrev_i32_e32 v21, 31, v20
	v_lshl_add_u64 v[20:21], v[20:21], 3, s[46:47]
	global_store_dwordx2 v[20:21], v[28:29], off
	v_add_u32_e32 v20, 0x3c00, v14
	v_add_u32_e32 v14, 0x3e00, v14
	v_ashrrev_i32_e32 v15, 31, v14
	v_ashrrev_i32_e32 v21, 31, v20
	v_lshl_add_u64 v[14:15], v[14:15], 3, s[46:47]
	v_lshl_add_u64 v[20:21], v[20:21], 3, s[46:47]
	global_store_dwordx2 v[14:15], v[18:19], off
	v_mov_b32_e32 v14, v182
	global_store_dwordx2 v[20:21], v[38:39], off
	s_barrier
	v_mov_b32_e32 v40, v169
	v_ashrrev_i32_e32 v15, 31, v14
	v_lshl_add_u64 v[18:19], v[14:15], 2, s[64:65]
	v_add_co_u32_e32 v28, vcc, s0, v18
	s_movk_i32 s0, 0x2000
	s_nop 0
	v_addc_co_u32_e32 v29, vcc, 0, v19, vcc
	v_add_co_u32_e32 v22, vcc, s0, v18
	s_movk_i32 s0, 0x6000
	s_nop 0
	v_addc_co_u32_e32 v23, vcc, 0, v19, vcc
	v_add_co_u32_e32 v30, vcc, s78, v18
	global_load_dword v20, v[18:19], off
	global_load_dword v21, v[18:19], off offset:2048
	v_addc_co_u32_e32 v31, vcc, 0, v19, vcc
	v_add_co_u32_e32 v32, vcc, s43, v18
	v_mov_b32_e32 v15, v173
	s_nop 0
	v_addc_co_u32_e32 v33, vcc, 0, v19, vcc
	v_add_co_u32_e32 v34, vcc, s0, v18
	s_mov_b32 s0, 0x8000
	s_nop 0
	v_addc_co_u32_e32 v35, vcc, 0, v19, vcc
	v_add_co_u32_e32 v36, vcc, s0, v18
	s_mov_b32 s0, 0xa000
	s_nop 0
	v_addc_co_u32_e32 v37, vcc, 0, v19, vcc
	v_add_co_u32_e32 v38, vcc, s0, v18
	global_load_dword v26, v[22:23], off offset:-4096
	global_load_dword v24, v[22:23], off
	global_load_dword v25, v[22:23], off offset:2048
	s_nop 0
	global_load_dword v22, v[32:33], off offset:-4096
	v_addc_co_u32_e32 v39, vcc, 0, v19, vcc
	global_load_dword v43, v[32:33], off offset:2048
	global_load_dword v46, v[34:35], off offset:-4096
	global_load_dword v48, v[36:37], off
	global_load_dword v49, v[36:37], off offset:2048
	global_load_dword v62, v[34:35], off
	global_load_dword v63, v[34:35], off offset:2048
	s_nop 0
	global_load_dword v34, v[38:39], off offset:-4096
	global_load_dword v64, v[36:37], off offset:-4096
	s_mov_b32 s0, 0x9000
	v_add_co_u32_e32 v36, vcc, s0, v18
	s_movk_i32 s0, 0x5000
	s_nop 0
	v_addc_co_u32_e32 v37, vcc, 0, v19, vcc
	global_load_dword v27, v[28:29], off offset:2048
	global_load_dword v35, v[36:37], off offset:2048
	v_add_co_u32_e32 v28, vcc, s0, v18
	s_mov_b32 s0, 0xb000
	s_nop 0
	v_addc_co_u32_e32 v29, vcc, 0, v19, vcc
	global_load_dword v66, v[38:39], off
	global_load_dword v67, v[38:39], off offset:2048
	v_add_co_u32_e32 v36, vcc, s0, v18
	s_mov_b32 s0, 0xc000
	s_nop 0
	v_addc_co_u32_e32 v37, vcc, 0, v19, vcc
	v_add_co_u32_e32 v38, vcc, s0, v18
	s_movk_i32 s0, 0x7000
	s_nop 0
	v_addc_co_u32_e32 v39, vcc, 0, v19, vcc
	global_load_dword v68, v[38:39], off offset:-4096
	global_load_dword v23, v[30:31], off offset:2048
	global_load_dword v69, v[36:37], off offset:2048
	v_add_co_u32_e32 v30, vcc, s0, v18
	s_mov_b32 s0, 0xe000
	s_nop 0
	v_addc_co_u32_e32 v31, vcc, 0, v19, vcc
	global_load_dword v47, v[28:29], off offset:2048
	global_load_dword v65, v[30:31], off offset:2048
	global_load_dword v42, v[32:33], off
	s_nop 0
	global_load_dword v30, v[38:39], off
	global_load_dword v31, v[38:39], off offset:2048
	v_add_co_u32_e32 v28, vcc, s0, v18
	s_mov_b32 s0, 0xd000
	s_nop 0
	v_addc_co_u32_e32 v29, vcc, 0, v19, vcc
	global_load_dword v32, v[28:29], off offset:-4096
	v_add_co_u32_e32 v36, vcc, s0, v18
	s_mov_b32 s0, 0xf000
	s_nop 0
	v_addc_co_u32_e32 v37, vcc, 0, v19, vcc
	global_load_dword v33, v[36:37], off offset:2048
	global_load_dword v38, v[28:29], off
	global_load_dword v39, v[28:29], off offset:2048
	v_add_co_u32_e32 v18, vcc, s0, v18
	v_mov_b32_e32 v36, v165
	s_nop 0
	v_addc_co_u32_e32 v19, vcc, 0, v19, vcc
	global_load_dword v70, v[18:19], off
	global_load_dword v71, v[18:19], off offset:2048
	v_mov_b32_e32 v28, v167
	v_mov_b32_e32 v45, v11
	v_mov_b32_e32 v10, v171
	s_waitcnt vmcnt(22)
	v_sub_f32_e32 v44, v21, v49
	v_mov_b32_e32 v13, v44
	v_pk_mul_f32 v[50:51], v[12:13], v[78:79] op_sel_hi:[1,0] neg_lo:[0,1] neg_hi:[0,1]
	v_sub_f32_e32 v10, v20, v48
	v_pk_fma_f32 v[44:45], v[44:45], v[72:73], v[50:51] op_sel_hi:[1,0,1]
	s_waitcnt vmcnt(19)
	v_sub_f32_e32 v50, v26, v34
	v_mov_b32_e32 v13, v50
	v_mov_b32_e32 v51, v11
	v_pk_mul_f32 v[52:53], v[12:13], v[40:41] op_sel_hi:[1,0] neg_lo:[0,1] neg_hi:[0,1]
	v_pk_add_f32 v[20:21], v[20:21], v[48:49]
	v_pk_fma_f32 v[50:51], v[50:51], v[36:37], v[52:53] op_sel_hi:[1,0,1]
	s_waitcnt vmcnt(16)
	v_sub_f32_e32 v52, v27, v35
	v_mov_b32_e32 v13, v52
	v_mov_b32_e32 v53, v11
	v_pk_mul_f32 v[54:55], v[12:13], v[76:77] op_sel_hi:[1,0] neg_lo:[0,1] neg_hi:[0,1]
	v_pk_add_f32 v[26:27], v[26:27], v[34:35]
	v_pk_fma_f32 v[54:55], v[52:53], v[74:75], v[54:55] op_sel_hi:[1,0,1]
	s_waitcnt vmcnt(15)
	v_sub_f32_e32 v52, v24, v66
	v_mov_b32_e32 v13, v52
	v_pk_mul_f32 v[56:57], v[12:13], v[28:29] op_sel_hi:[1,0] neg_lo:[0,1] neg_hi:[0,1]
	s_waitcnt vmcnt(6)
	v_sub_f32_e32 v82, v43, v31
	v_pk_fma_f32 v[56:57], v[52:53], v[28:29], v[56:57] op_sel_hi:[1,0,1]
	v_sub_f32_e32 v52, v25, v67
	v_pk_mul_f32 v[58:59], v[52:53], v[76:77] op_sel_hi:[1,0]
	v_mov_b32_e32 v13, v52
	v_sub_f32_e32 v52, v22, v68
	v_pk_fma_f32 v[60:61], v[12:13], v[74:75], v[58:59] op_sel_hi:[1,0,1] neg_lo:[0,1,0] neg_hi:[0,1,0]
	v_pk_mul_f32 v[58:59], v[52:53], v[40:41] op_sel_hi:[1,0]
	v_mov_b32_e32 v13, v52
	v_sub_f32_e32 v52, v23, v69
	v_pk_fma_f32 v[58:59], v[12:13], v[36:37], v[58:59] op_sel_hi:[1,0,1] neg_lo:[0,1,0] neg_hi:[0,1,0]
	v_pk_mul_f32 v[80:81], v[52:53], v[78:79] op_sel_hi:[1,0]
	v_mov_b32_e32 v13, v52
	v_pk_fma_f32 v[52:53], v[12:13], v[72:73], v[80:81] op_sel_hi:[1,0,1] neg_lo:[0,1,0] neg_hi:[0,1,0]
	v_sub_f32_e32 v13, v42, v30
	v_xor_b32_e32 v81, 0x80000000, v13
	v_pk_mul_f32 v[84:85], v[82:83], v[78:79] op_sel_hi:[1,0] neg_lo:[0,1] neg_hi:[0,1]
	v_mov_b32_e32 v13, v82
	v_pk_fma_f32 v[82:83], v[12:13], v[72:73], v[84:85] op_sel_hi:[1,0,1] neg_lo:[0,1,0] neg_hi:[0,1,0]
	s_waitcnt vmcnt(5)
	v_sub_f32_e32 v84, v46, v32
	v_mov_b32_e32 v85, v11
	v_pk_mul_f32 v[86:87], v[84:85], v[40:41] op_sel_hi:[1,0] neg_lo:[0,1] neg_hi:[0,1]
	v_mov_b32_e32 v13, v84
	v_pk_fma_f32 v[84:85], v[12:13], v[36:37], v[86:87] op_sel_hi:[1,0,1] neg_lo:[0,1,0] neg_hi:[0,1,0]
	s_waitcnt vmcnt(4)
	v_sub_f32_e32 v86, v47, v33
	v_mov_b32_e32 v87, v11
	v_pk_mul_f32 v[88:89], v[86:87], v[76:77] op_sel_hi:[1,0] neg_lo:[0,1] neg_hi:[0,1]
	v_mov_b32_e32 v13, v86
	v_pk_fma_f32 v[86:87], v[12:13], v[74:75], v[88:89] op_sel_hi:[1,0,1] neg_lo:[0,1,0] neg_hi:[0,1,0]
	s_waitcnt vmcnt(3)
	v_sub_f32_e32 v88, v62, v38
	v_mov_b32_e32 v13, v88
	v_mov_b32_e32 v89, v11
	v_pk_mul_f32 v[90:91], v[12:13], v[28:29] op_sel_hi:[1,0] neg_lo:[0,1] neg_hi:[0,1]
	v_pk_add_f32 v[30:31], v[42:43], v[30:31]
	v_pk_fma_f32 v[88:89], v[88:89], v[28:29], v[90:91] op_sel_hi:[1,0,1] neg_lo:[0,1,0] neg_hi:[0,1,0]
	s_waitcnt vmcnt(2)
	v_sub_f32_e32 v90, v63, v39
	v_mov_b32_e32 v13, v90
	v_mov_b32_e32 v91, v11
	v_pk_mul_f32 v[76:77], v[12:13], v[76:77] op_sel_hi:[1,0] neg_lo:[0,1] neg_hi:[0,1]
	v_pk_add_f32 v[42:43], v[20:21], v[30:31] neg_lo:[0,1] neg_hi:[0,1]
	v_pk_fma_f32 v[74:75], v[90:91], v[74:75], v[76:77] op_sel_hi:[1,0,1] neg_lo:[0,1,0] neg_hi:[0,1,0]
	s_waitcnt vmcnt(1)
	v_sub_f32_e32 v76, v64, v70
	v_mov_b32_e32 v13, v76
	v_mov_b32_e32 v77, v11
	v_pk_mul_f32 v[90:91], v[12:13], v[40:41] op_sel_hi:[1,0] neg_lo:[0,1] neg_hi:[0,1]
	v_pk_add_f32 v[32:33], v[46:47], v[32:33]
	v_pk_fma_f32 v[76:77], v[76:77], v[36:37], v[90:91] op_sel_hi:[1,0,1] neg_lo:[0,1,0] neg_hi:[0,1,0]
	s_waitcnt vmcnt(0)
	v_sub_f32_e32 v90, v65, v71
	v_mov_b32_e32 v13, v90
	v_pk_mul_f32 v[78:79], v[12:13], v[78:79] op_sel_hi:[1,0] neg_lo:[0,1] neg_hi:[0,1]
	v_mov_b32_e32 v13, v43
	v_mov_b32_e32 v46, v42
	v_pk_add_f32 v[20:21], v[20:21], v[30:31]
	v_mov_b32_e32 v30, v43
	v_mov_b32_e32 v31, v11
	v_pk_mul_f32 v[42:43], v[12:13], v[40:41] op_sel_hi:[1,0] neg_lo:[0,1] neg_hi:[0,1]
	v_pk_add_f32 v[34:35], v[62:63], v[38:39]
	v_pk_fma_f32 v[62:63], v[30:31], v[36:37], v[42:43] op_sel_hi:[1,0,1]
	v_pk_add_f32 v[30:31], v[26:27], v[32:33] neg_lo:[0,1] neg_hi:[0,1]
	v_pk_add_f32 v[24:25], v[24:25], v[66:67]
	v_mov_b32_e32 v13, v30
	v_mov_b32_e32 v42, v30
	v_pk_mul_f32 v[48:49], v[12:13], v[28:29] op_sel_hi:[1,0] neg_lo:[0,1] neg_hi:[0,1]
	v_pk_add_f32 v[26:27], v[26:27], v[32:33]
	v_mov_b32_e32 v32, v31
	v_mov_b32_e32 v33, v11
	v_mov_b32_e32 v13, v31
	v_pk_add_f32 v[30:31], v[24:25], v[34:35] neg_lo:[0,1] neg_hi:[0,1]
	v_pk_add_f32 v[22:23], v[22:23], v[68:69]
	v_pk_add_f32 v[38:39], v[64:65], v[70:71]
	v_pk_mul_f32 v[32:33], v[32:33], v[40:41] op_sel_hi:[1,0]
	v_pk_add_f32 v[24:25], v[24:25], v[34:35]
	v_mov_b32_e32 v34, v31
	v_mov_b32_e32 v35, v11
	v_pk_fma_f32 v[32:33], v[12:13], v[36:37], v[32:33] op_sel_hi:[1,0,1] neg_lo:[0,1,0] neg_hi:[0,1,0]
	v_xor_b32_e32 v67, 0x80000000, v30
	v_pk_mul_f32 v[34:35], v[34:35], v[40:41] op_sel_hi:[1,0] neg_lo:[0,1] neg_hi:[0,1]
	v_mov_b32_e32 v13, v31
	v_pk_add_f32 v[30:31], v[22:23], v[38:39] neg_lo:[0,1] neg_hi:[0,1]
	v_mov_b32_e32 v43, v11
	v_pk_fma_f32 v[68:69], v[12:13], v[36:37], v[34:35] op_sel_hi:[1,0,1] neg_lo:[0,1,0] neg_hi:[0,1,0]
	v_mov_b32_e32 v13, v30
	v_pk_fma_f32 v[64:65], v[42:43], v[28:29], v[48:49] op_sel_hi:[1,0,1]
	v_mov_b32_e32 v34, v30
	v_mov_b32_e32 v35, v11
	v_pk_mul_f32 v[42:43], v[12:13], v[28:29] op_sel_hi:[1,0] neg_lo:[0,1] neg_hi:[0,1]
	v_mov_b32_e32 v13, v31
	v_pk_fma_f32 v[70:71], v[34:35], v[28:29], v[42:43] op_sel_hi:[1,0,1] neg_lo:[0,1,0] neg_hi:[0,1,0]
	v_mov_b32_e32 v34, v31
	v_pk_mul_f32 v[30:31], v[12:13], v[40:41] op_sel_hi:[1,0] neg_lo:[0,1] neg_hi:[0,1]
	v_pk_add_f32 v[22:23], v[22:23], v[38:39]
	v_pk_fma_f32 v[38:39], v[34:35], v[36:37], v[30:31] op_sel_hi:[1,0,1] neg_lo:[0,1,0] neg_hi:[0,1,0]
	v_pk_add_f32 v[30:31], v[20:21], v[24:25] neg_lo:[0,1] neg_hi:[0,1]
	v_pk_add_f32 v[20:21], v[20:21], v[24:25]
	v_mov_b32_e32 v13, v31
	v_mov_b32_e32 v42, v30
	v_mov_b32_e32 v24, v31
	v_mov_b32_e32 v25, v11
	v_pk_mul_f32 v[30:31], v[12:13], v[28:29] op_sel_hi:[1,0] neg_lo:[0,1] neg_hi:[0,1]
	v_mov_b32_e32 v91, v11
	v_pk_fma_f32 v[30:31], v[24:25], v[28:29], v[30:31] op_sel_hi:[1,0,1]
	v_pk_add_f32 v[24:25], v[26:27], v[22:23] neg_lo:[0,1] neg_hi:[0,1]
	v_pk_fma_f32 v[72:73], v[90:91], v[72:73], v[78:79] op_sel_hi:[1,0,1] neg_lo:[0,1,0] neg_hi:[0,1,0]
	v_mov_b32_e32 v13, v25
	v_xor_b32_e32 v79, 0x80000000, v24
	v_pk_add_f32 v[22:23], v[26:27], v[22:23]
	v_mov_b32_e32 v26, v25
	v_mov_b32_e32 v27, v11
	v_pk_mul_f32 v[24:25], v[12:13], v[28:29] op_sel_hi:[1,0] neg_lo:[0,1] neg_hi:[0,1]
	v_pk_add_f32 v[34:35], v[20:21], v[22:23]
	v_pk_fma_f32 v[26:27], v[26:27], v[28:29], v[24:25] op_sel_hi:[1,0,1] neg_lo:[0,1,0] neg_hi:[0,1,0]
	v_pk_add_f32 v[24:25], v[20:21], v[22:23] neg_lo:[0,1] neg_hi:[0,1]
	v_mov_b32_e32 v43, v11
	v_pk_add_f32 v[20:21], v[24:25], 0 neg_lo:[1,1] neg_hi:[1,1]
	v_mov_b32_e32 v78, v11
	v_mov_b32_e32 v90, v24
	v_mov_b32_e32 v20, v11
	v_pk_add_f32 v[48:49], v[90:91], v[20:21]
	v_pk_add_f32 v[24:25], v[90:91], v[20:21] neg_lo:[0,1] neg_hi:[0,1]
	v_pk_add_f32 v[20:21], v[42:43], v[78:79]
	v_pk_add_f32 v[22:23], v[42:43], v[78:79] neg_lo:[0,1] neg_hi:[0,1]
	v_pk_add_f32 v[42:43], v[30:31], v[26:27]
	v_pk_add_f32 v[26:27], v[30:31], v[26:27] neg_lo:[0,1] neg_hi:[0,1]
	v_mov_b32_e32 v47, v11
	v_mov_b32_e32 v66, v11
	v_xor_b32_e32 v79, 0x80000000, v26
	v_mov_b32_e32 v78, v27
	v_pk_add_f32 v[26:27], v[62:63], v[68:69]
	v_pk_add_f32 v[62:63], v[62:63], v[68:69] neg_lo:[0,1] neg_hi:[0,1]
	v_pk_add_f32 v[90:91], v[20:21], v[42:43]
	v_pk_add_f32 v[30:31], v[20:21], v[42:43] neg_lo:[0,1] neg_hi:[0,1]
	v_pk_add_f32 v[42:43], v[22:23], v[78:79]
	v_pk_add_f32 v[20:21], v[22:23], v[78:79] neg_lo:[0,1] neg_hi:[0,1]
	v_pk_add_f32 v[22:23], v[46:47], v[66:67]
	v_pk_add_f32 v[46:47], v[46:47], v[66:67] neg_lo:[0,1] neg_hi:[0,1]
	v_pk_mul_f32 v[66:67], v[28:29], v[62:63] op_sel:[0,1] op_sel_hi:[0,0] neg_lo:[1,1] neg_hi:[1,0]
	v_pk_fma_f32 v[66:67], v[28:29], v[62:63], v[66:67] op_sel_hi:[0,1,1]
	v_pk_add_f32 v[62:63], v[64:65], v[70:71]
	v_pk_add_f32 v[64:65], v[64:65], v[70:71] neg_lo:[0,1] neg_hi:[0,1]
	v_mov_b32_e32 v80, v11
	v_xor_b32_e32 v69, 0x80000000, v64
	v_mov_b32_e32 v68, v65
	v_pk_add_f32 v[64:65], v[32:33], v[38:39]
	v_pk_add_f32 v[32:33], v[32:33], v[38:39] neg_lo:[0,1] neg_hi:[0,1]
	v_pk_add_f32 v[78:79], v[44:45], v[82:83]
	v_pk_mul_f32 v[38:39], v[28:29], v[32:33] op_sel:[0,1] op_sel_hi:[0,0] neg_lo:[1,1] neg_hi:[1,0]
	v_pk_fma_f32 v[32:33], v[28:29], v[32:33], v[38:39] op_sel_hi:[0,1,1] neg_lo:[1,0,0] neg_hi:[1,0,0]
	v_pk_add_f32 v[38:39], v[22:23], v[62:63]
	v_pk_add_f32 v[22:23], v[22:23], v[62:63] neg_lo:[0,1] neg_hi:[0,1]
	v_pk_add_f32 v[62:63], v[26:27], v[64:65]
	v_pk_add_f32 v[26:27], v[26:27], v[64:65] neg_lo:[0,1] neg_hi:[0,1]
	v_pk_add_f32 v[70:71], v[38:39], v[62:63]
	v_pk_add_f32 v[38:39], v[38:39], v[62:63] neg_lo:[0,1] neg_hi:[0,1]
	v_pk_add_f32 v[62:63], v[22:23], v[26:27] op_sel:[0,1] op_sel_hi:[1,0] neg_hi:[0,1]
	v_pk_add_f32 v[26:27], v[22:23], v[26:27] op_sel:[0,1] op_sel_hi:[1,0] neg_lo:[0,1]
	v_pk_add_f32 v[22:23], v[46:47], v[68:69]
	v_pk_add_f32 v[64:65], v[46:47], v[68:69] neg_lo:[0,1] neg_hi:[0,1]
	v_pk_add_f32 v[46:47], v[66:67], v[32:33]
	v_pk_add_f32 v[32:33], v[66:67], v[32:33] neg_lo:[0,1] neg_hi:[0,1]
	v_pk_add_f32 v[44:45], v[44:45], v[82:83] neg_lo:[0,1] neg_hi:[0,1]
	v_xor_b32_e32 v67, 0x80000000, v32
	v_mov_b32_e32 v66, v33
	v_pk_add_f32 v[68:69], v[22:23], v[46:47]
	v_pk_add_f32 v[32:33], v[22:23], v[46:47] neg_lo:[0,1] neg_hi:[0,1]
	v_pk_add_f32 v[46:47], v[64:65], v[66:67]
	v_pk_add_f32 v[22:23], v[64:65], v[66:67] neg_lo:[0,1] neg_hi:[0,1]
	v_pk_add_f32 v[64:65], v[10:11], v[80:81]
	v_pk_add_f32 v[66:67], v[10:11], v[80:81] neg_lo:[0,1] neg_hi:[0,1]
	v_pk_mul_f32 v[80:81], v[40:41], v[44:45] op_sel:[0,1] op_sel_hi:[0,0] neg_lo:[1,1] neg_hi:[1,0]
	v_pk_fma_f32 v[44:45], v[36:37], v[44:45], v[80:81] op_sel_hi:[0,1,1]
	v_pk_add_f32 v[80:81], v[50:51], v[84:85]
	v_pk_add_f32 v[50:51], v[50:51], v[84:85] neg_lo:[0,1] neg_hi:[0,1]
	v_add_f32_e32 v10, v34, v35
	v_pk_mul_f32 v[82:83], v[28:29], v[50:51] op_sel:[0,1] op_sel_hi:[0,0] neg_lo:[1,1] neg_hi:[1,0]
	v_pk_fma_f32 v[82:83], v[28:29], v[50:51], v[82:83] op_sel_hi:[0,1,1]
	v_pk_add_f32 v[50:51], v[54:55], v[86:87]
	v_pk_add_f32 v[54:55], v[54:55], v[86:87] neg_lo:[0,1] neg_hi:[0,1]
	v_pk_fma_f32 v[16:17], v[10:11], s[94:95], v[16:17] op_sel_hi:[0,1,1]
	v_pk_mul_f32 v[84:85], v[36:37], v[54:55] op_sel:[0,1] op_sel_hi:[0,0] neg_lo:[1,1] neg_hi:[1,0]
	v_pk_fma_f32 v[84:85], v[40:41], v[54:55], v[84:85] op_sel_hi:[0,1,1]
	v_pk_add_f32 v[54:55], v[56:57], v[88:89]
	v_pk_add_f32 v[56:57], v[56:57], v[88:89] neg_lo:[0,1] neg_hi:[0,1]
	v_lshl_add_u32 v13, v15, 3, 0
	v_xor_b32_e32 v87, 0x80000000, v56
	v_mov_b32_e32 v86, v57
	v_pk_add_f32 v[56:57], v[60:61], v[74:75]
	v_pk_add_f32 v[60:61], v[60:61], v[74:75] neg_lo:[0,1] neg_hi:[0,1]
	ds_write_b64 v13, v[16:17]
	v_pk_mul_f32 v[74:75], v[36:37], v[60:61] op_sel:[0,1] op_sel_hi:[0,0] neg_lo:[1,1] neg_hi:[1,0]
	v_pk_fma_f32 v[60:61], v[40:41], v[60:61], v[74:75] op_sel_hi:[0,1,1] neg_lo:[1,0,0] neg_hi:[1,0,0]
	v_pk_add_f32 v[74:75], v[58:59], v[76:77]
	v_pk_add_f32 v[58:59], v[58:59], v[76:77] neg_lo:[0,1] neg_hi:[0,1]
	v_pk_fma_f32 v[16:17], v[178:179], s[90:91], v[178:179] op_sel:[1,0,0] op_sel_hi:[0,1,1]
	v_pk_mul_f32 v[76:77], v[28:29], v[58:59] op_sel:[0,1] op_sel_hi:[0,0] neg_lo:[1,1] neg_hi:[1,0]
	v_pk_fma_f32 v[58:59], v[28:29], v[58:59], v[76:77] op_sel_hi:[0,1,1] neg_lo:[1,0,0] neg_hi:[1,0,0]
	v_pk_add_f32 v[76:77], v[52:53], v[72:73]
	v_pk_add_f32 v[52:53], v[52:53], v[72:73] neg_lo:[0,1] neg_hi:[0,1]
	v_pk_mul_f32 v[40:41], v[40:41], v[52:53] op_sel:[0,1] op_sel_hi:[0,0] neg_lo:[1,1] neg_hi:[1,0]
	v_pk_fma_f32 v[52:53], v[36:37], v[52:53], v[40:41] op_sel_hi:[0,1,1] neg_lo:[1,0,0] neg_hi:[1,0,0]
	v_pk_add_f32 v[36:37], v[64:65], v[54:55]
	v_pk_add_f32 v[64:65], v[64:65], v[54:55] neg_lo:[0,1] neg_hi:[0,1]
	v_pk_add_f32 v[54:55], v[78:79], v[56:57] neg_lo:[0,1] neg_hi:[0,1]
	v_pk_add_f32 v[40:41], v[56:57], v[78:79]
	v_pk_mul_f32 v[56:57], v[28:29], v[54:55] op_sel:[0,1] op_sel_hi:[0,0] neg_lo:[1,1] neg_hi:[1,0]
	v_pk_add_f32 v[72:73], v[80:81], v[74:75] neg_lo:[0,1] neg_hi:[0,1]
	v_pk_fma_f32 v[56:57], v[28:29], v[54:55], v[56:57] op_sel_hi:[0,1,1]
	v_pk_add_f32 v[54:55], v[80:81], v[74:75]
	v_xor_b32_e32 v75, 0x80000000, v72
	v_mov_b32_e32 v74, v73
	v_pk_add_f32 v[72:73], v[50:51], v[76:77]
	v_pk_add_f32 v[50:51], v[50:51], v[76:77] neg_lo:[0,1] neg_hi:[0,1]
	v_pk_mul_f32 v[76:77], v[28:29], v[50:51] op_sel:[0,1] op_sel_hi:[0,0] neg_lo:[1,1] neg_hi:[1,0]
	v_pk_fma_f32 v[50:51], v[28:29], v[50:51], v[76:77] op_sel_hi:[0,1,1] neg_lo:[1,0,0] neg_hi:[1,0,0]
	v_pk_add_f32 v[76:77], v[36:37], v[54:55]
	v_pk_add_f32 v[36:37], v[36:37], v[54:55] neg_lo:[0,1] neg_hi:[0,1]
	v_pk_add_f32 v[54:55], v[40:41], v[72:73]
	v_pk_add_f32 v[40:41], v[40:41], v[72:73] neg_lo:[0,1] neg_hi:[0,1]
	v_pk_add_f32 v[78:79], v[76:77], v[54:55]
	v_pk_add_f32 v[54:55], v[76:77], v[54:55] neg_lo:[0,1] neg_hi:[0,1]
	v_pk_add_f32 v[76:77], v[36:37], v[40:41] op_sel:[0,1] op_sel_hi:[1,0] neg_hi:[0,1]
	v_pk_add_f32 v[40:41], v[36:37], v[40:41] op_sel:[0,1] op_sel_hi:[1,0] neg_lo:[0,1]
	v_pk_add_f32 v[72:73], v[56:57], v[50:51]
	v_pk_add_f32 v[50:51], v[56:57], v[50:51] neg_lo:[0,1] neg_hi:[0,1]
	v_pk_add_f32 v[36:37], v[64:65], v[74:75]
	v_pk_add_f32 v[64:65], v[64:65], v[74:75] neg_lo:[0,1] neg_hi:[0,1]
	v_xor_b32_e32 v57, 0x80000000, v50
	v_mov_b32_e32 v56, v51
	v_pk_add_f32 v[74:75], v[36:37], v[72:73]
	v_pk_add_f32 v[50:51], v[36:37], v[72:73] neg_lo:[0,1] neg_hi:[0,1]
	v_pk_add_f32 v[72:73], v[64:65], v[56:57]
	v_pk_add_f32 v[36:37], v[64:65], v[56:57] neg_lo:[0,1] neg_hi:[0,1]
	v_pk_add_f32 v[56:57], v[66:67], v[86:87]
	v_pk_add_f32 v[64:65], v[66:67], v[86:87] neg_lo:[0,1] neg_hi:[0,1]
	v_pk_add_f32 v[66:67], v[60:61], v[44:45]
	v_pk_add_f32 v[44:45], v[44:45], v[60:61] neg_lo:[0,1] neg_hi:[0,1]
	v_pk_mul_f32 v[60:61], v[28:29], v[44:45] op_sel:[0,1] op_sel_hi:[0,0] neg_lo:[1,1] neg_hi:[1,0]
	v_pk_fma_f32 v[60:61], v[28:29], v[44:45], v[60:61] op_sel_hi:[0,1,1]
	v_pk_add_f32 v[44:45], v[82:83], v[58:59]
	v_pk_add_f32 v[58:59], v[82:83], v[58:59] neg_lo:[0,1] neg_hi:[0,1]
	v_xor_b32_e32 v81, 0x80000000, v58
	v_mov_b32_e32 v80, v59
	v_pk_add_f32 v[58:59], v[84:85], v[52:53]
	v_pk_add_f32 v[52:53], v[84:85], v[52:53] neg_lo:[0,1] neg_hi:[0,1]
	v_pk_mul_f32 v[82:83], v[28:29], v[52:53] op_sel:[0,1] op_sel_hi:[0,0] neg_lo:[1,1] neg_hi:[1,0]
	v_pk_fma_f32 v[28:29], v[28:29], v[52:53], v[82:83] op_sel_hi:[0,1,1] neg_lo:[1,0,0] neg_hi:[1,0,0]
	v_pk_add_f32 v[52:53], v[56:57], v[44:45]
	v_pk_add_f32 v[44:45], v[56:57], v[44:45] neg_lo:[0,1] neg_hi:[0,1]
	v_pk_add_f32 v[56:57], v[66:67], v[58:59]
	v_pk_add_f32 v[58:59], v[66:67], v[58:59] neg_lo:[0,1] neg_hi:[0,1]
	v_pk_add_f32 v[82:83], v[44:45], v[58:59] op_sel:[0,1] op_sel_hi:[1,0] neg_hi:[0,1]
	v_pk_add_f32 v[44:45], v[44:45], v[58:59] op_sel:[0,1] op_sel_hi:[1,0] neg_lo:[0,1]
	v_pk_add_f32 v[66:67], v[60:61], v[28:29]
	v_pk_add_f32 v[28:29], v[60:61], v[28:29] neg_lo:[0,1] neg_hi:[0,1]
	v_pk_add_f32 v[58:59], v[52:53], v[56:57]
	v_pk_add_f32 v[56:57], v[52:53], v[56:57] neg_lo:[0,1] neg_hi:[0,1]
	v_pk_add_f32 v[52:53], v[64:65], v[80:81]
	v_pk_add_f32 v[64:65], v[64:65], v[80:81] neg_lo:[0,1] neg_hi:[0,1]
	v_pk_add_f32 v[80:81], v[52:53], v[66:67]
	v_pk_add_f32 v[52:53], v[52:53], v[66:67] neg_lo:[0,1] neg_hi:[0,1]
	v_pk_add_f32 v[66:67], v[64:65], v[28:29] op_sel:[0,1] op_sel_hi:[1,0] neg_hi:[0,1]
	v_pk_add_f32 v[28:29], v[64:65], v[28:29] op_sel:[0,1] op_sel_hi:[1,0] neg_lo:[0,1]
	v_pk_mul_f32 v[60:61], v[16:17], v[78:79] op_sel:[1,1] op_sel_hi:[0,1] neg_lo:[0,1]
	v_pk_fma_f32 v[60:61], v[16:17], v[78:79], v[60:61] op_sel_hi:[1,0,1]
	ds_write_b64 v13, v[60:61] offset:4224
	v_pk_mul_f32 v[60:61], v[178:179], v[16:17] op_sel:[1,1] op_sel_hi:[0,1] neg_lo:[0,1]
	v_pk_fma_f32 v[16:17], v[178:179], v[16:17], v[60:61] op_sel_hi:[1,0,1]
	v_pk_mul_f32 v[60:61], v[16:17], v[70:71] op_sel:[1,1] op_sel_hi:[0,1] neg_lo:[0,1]
	v_pk_fma_f32 v[60:61], v[16:17], v[70:71], v[60:61] op_sel_hi:[1,0,1]
	ds_write_b64 v13, v[60:61] offset:8448
	v_pk_mul_f32 v[60:61], v[178:179], v[16:17] op_sel:[1,1] op_sel_hi:[0,1] neg_lo:[0,1]
	v_pk_fma_f32 v[16:17], v[178:179], v[16:17], v[60:61] op_sel_hi:[1,0,1]
	v_pk_mul_f32 v[60:61], v[16:17], v[58:59] op_sel:[1,1] op_sel_hi:[0,1] neg_lo:[0,1]
	v_pk_fma_f32 v[58:59], v[16:17], v[58:59], v[60:61] op_sel_hi:[1,0,1]
	ds_write_b64 v13, v[58:59] offset:12672
	v_pk_mul_f32 v[58:59], v[178:179], v[16:17] op_sel:[1,1] op_sel_hi:[0,1] neg_lo:[0,1]
	v_pk_fma_f32 v[16:17], v[178:179], v[16:17], v[58:59] op_sel_hi:[1,0,1]
	v_pk_mul_f32 v[58:59], v[90:91], v[16:17] op_sel:[1,1] op_sel_hi:[1,0] neg_lo:[1,0]
	v_pk_fma_f32 v[58:59], v[90:91], v[16:17], v[58:59] op_sel_hi:[0,1,1]
	ds_write_b64 v13, v[58:59] offset:16896
	v_pk_mul_f32 v[58:59], v[178:179], v[16:17] op_sel:[1,1] op_sel_hi:[0,1] neg_lo:[0,1]
	v_pk_fma_f32 v[16:17], v[178:179], v[16:17], v[58:59] op_sel_hi:[1,0,1]
	v_pk_mul_f32 v[58:59], v[16:17], v[74:75] op_sel:[1,1] op_sel_hi:[0,1] neg_lo:[0,1]
	v_pk_fma_f32 v[58:59], v[16:17], v[74:75], v[58:59] op_sel_hi:[1,0,1]
	ds_write_b64 v13, v[58:59] offset:21120
	v_pk_mul_f32 v[58:59], v[178:179], v[16:17] op_sel:[1,1] op_sel_hi:[0,1] neg_lo:[0,1]
	v_pk_fma_f32 v[16:17], v[178:179], v[16:17], v[58:59] op_sel_hi:[1,0,1]
	v_pk_mul_f32 v[58:59], v[68:69], v[16:17] op_sel:[1,1] op_sel_hi:[1,0] neg_lo:[1,0]
	v_pk_fma_f32 v[58:59], v[68:69], v[16:17], v[58:59] op_sel_hi:[0,1,1]
	ds_write_b64 v13, v[58:59] offset:25344
	v_pk_mul_f32 v[58:59], v[178:179], v[16:17] op_sel:[1,1] op_sel_hi:[0,1] neg_lo:[0,1]
	v_pk_fma_f32 v[16:17], v[178:179], v[16:17], v[58:59] op_sel_hi:[1,0,1]
	v_pk_mul_f32 v[58:59], v[80:81], v[16:17] op_sel:[1,1] op_sel_hi:[1,0] neg_lo:[1,0]
	v_pk_fma_f32 v[58:59], v[80:81], v[16:17], v[58:59] op_sel_hi:[0,1,1]
	ds_write_b64 v13, v[58:59] offset:29568
	v_pk_mul_f32 v[58:59], v[178:179], v[16:17] op_sel:[1,1] op_sel_hi:[0,1] neg_lo:[0,1]
	v_pk_fma_f32 v[16:17], v[178:179], v[16:17], v[58:59] op_sel_hi:[1,0,1]
	v_pk_mul_f32 v[58:59], v[48:49], v[16:17] op_sel:[1,1] op_sel_hi:[1,0] neg_lo:[1,0]
	v_pk_fma_f32 v[48:49], v[48:49], v[16:17], v[58:59] op_sel_hi:[0,1,1]
	ds_write_b64 v13, v[48:49] offset:33792
	v_pk_mul_f32 v[48:49], v[178:179], v[16:17] op_sel:[1,1] op_sel_hi:[0,1] neg_lo:[0,1]
	v_pk_fma_f32 v[16:17], v[178:179], v[16:17], v[48:49] op_sel_hi:[1,0,1]
	v_pk_mul_f32 v[48:49], v[76:77], v[16:17] op_sel:[1,1] op_sel_hi:[1,0] neg_lo:[1,0]
	v_pk_fma_f32 v[48:49], v[76:77], v[16:17], v[48:49] op_sel_hi:[0,1,1]
	ds_write_b64 v13, v[48:49] offset:38016
	v_pk_mul_f32 v[48:49], v[178:179], v[16:17] op_sel:[1,1] op_sel_hi:[0,1] neg_lo:[0,1]
	v_pk_fma_f32 v[16:17], v[178:179], v[16:17], v[48:49] op_sel_hi:[1,0,1]
	v_pk_mul_f32 v[48:49], v[62:63], v[16:17] op_sel:[1,1] op_sel_hi:[1,0] neg_lo:[1,0]
	v_pk_fma_f32 v[48:49], v[62:63], v[16:17], v[48:49] op_sel_hi:[0,1,1]
	ds_write_b64 v13, v[48:49] offset:42240
	v_pk_mul_f32 v[48:49], v[178:179], v[16:17] op_sel:[1,1] op_sel_hi:[0,1] neg_lo:[0,1]
	v_pk_fma_f32 v[16:17], v[178:179], v[16:17], v[48:49] op_sel_hi:[1,0,1]
	v_pk_mul_f32 v[48:49], v[82:83], v[16:17] op_sel:[1,1] op_sel_hi:[1,0] neg_lo:[1,0]
	v_pk_fma_f32 v[48:49], v[82:83], v[16:17], v[48:49] op_sel_hi:[0,1,1]
	ds_write_b64 v13, v[48:49] offset:46464
	v_pk_mul_f32 v[48:49], v[178:179], v[16:17] op_sel:[1,1] op_sel_hi:[0,1] neg_lo:[0,1]
	v_pk_fma_f32 v[16:17], v[178:179], v[16:17], v[48:49] op_sel_hi:[1,0,1]
	v_pk_mul_f32 v[48:49], v[42:43], v[16:17] op_sel:[1,1] op_sel_hi:[1,0] neg_lo:[1,0]
	v_pk_fma_f32 v[42:43], v[42:43], v[16:17], v[48:49] op_sel_hi:[0,1,1]
	ds_write_b64 v13, v[42:43] offset:50688
	v_pk_mul_f32 v[42:43], v[178:179], v[16:17] op_sel:[1,1] op_sel_hi:[0,1] neg_lo:[0,1]
	v_pk_fma_f32 v[16:17], v[178:179], v[16:17], v[42:43] op_sel_hi:[1,0,1]
	v_pk_mul_f32 v[42:43], v[72:73], v[16:17] op_sel:[1,1] op_sel_hi:[1,0] neg_lo:[1,0]
	v_pk_fma_f32 v[42:43], v[72:73], v[16:17], v[42:43] op_sel_hi:[0,1,1]
	ds_write_b64 v13, v[42:43] offset:54912
	v_pk_mul_f32 v[42:43], v[178:179], v[16:17] op_sel:[1,1] op_sel_hi:[0,1] neg_lo:[0,1]
	v_pk_fma_f32 v[16:17], v[178:179], v[16:17], v[42:43] op_sel_hi:[1,0,1]
	v_pk_mul_f32 v[42:43], v[46:47], v[16:17] op_sel:[1,1] op_sel_hi:[1,0] neg_lo:[1,0]
	v_pk_fma_f32 v[42:43], v[46:47], v[16:17], v[42:43] op_sel_hi:[0,1,1]
	ds_write_b64 v13, v[42:43] offset:59136
	v_pk_mul_f32 v[42:43], v[178:179], v[16:17] op_sel:[1,1] op_sel_hi:[0,1] neg_lo:[0,1]
	v_pk_fma_f32 v[16:17], v[178:179], v[16:17], v[42:43] op_sel_hi:[1,0,1]
	v_pk_mul_f32 v[42:43], v[66:67], v[16:17] op_sel:[1,1] op_sel_hi:[1,0] neg_lo:[1,0]
	v_pk_fma_f32 v[42:43], v[66:67], v[16:17], v[42:43] op_sel_hi:[0,1,1]
	ds_write_b64 v13, v[42:43] offset:63360
	v_pk_mul_f32 v[42:43], v[178:179], v[16:17] op_sel:[1,1] op_sel_hi:[0,1] neg_lo:[0,1]
	v_pk_fma_f32 v[16:17], v[178:179], v[16:17], v[42:43] op_sel_hi:[1,0,1]
	v_sub_f32_e32 v10, v34, v35
	v_pk_mul_f32 v[34:35], v[16:17], s[44:45]
	v_pk_fma_f32 v[34:35], v[10:11], v[16:17], v[34:35] op_sel:[0,0,1] op_sel_hi:[0,1,0]
	v_add_u32_e32 v10, 0x10800, v13
	ds_write_b64 v10, v[34:35]
	v_pk_mul_f32 v[34:35], v[178:179], v[16:17] op_sel:[1,1] op_sel_hi:[0,1] neg_lo:[0,1]
	v_pk_fma_f32 v[16:17], v[178:179], v[16:17], v[34:35] op_sel_hi:[1,0,1]
	v_pk_mul_f32 v[34:35], v[54:55], v[16:17] op_sel:[1,1] op_sel_hi:[1,0] neg_lo:[1,0]
	v_add_u32_e32 v10, 0x11880, v13
	v_pk_fma_f32 v[34:35], v[54:55], v[16:17], v[34:35] op_sel_hi:[0,1,1]
	ds_write_b64 v10, v[34:35]
	v_pk_mul_f32 v[34:35], v[178:179], v[16:17] op_sel:[1,1] op_sel_hi:[0,1] neg_lo:[0,1]
	v_pk_fma_f32 v[16:17], v[178:179], v[16:17], v[34:35] op_sel_hi:[1,0,1]
	v_pk_mul_f32 v[34:35], v[38:39], v[16:17] op_sel:[1,1] op_sel_hi:[1,0] neg_lo:[1,0]
	v_add_u32_e32 v10, 0x12900, v13
	v_pk_fma_f32 v[34:35], v[38:39], v[16:17], v[34:35] op_sel_hi:[0,1,1]
	ds_write_b64 v10, v[34:35]
	v_pk_mul_f32 v[34:35], v[178:179], v[16:17] op_sel:[1,1] op_sel_hi:[0,1] neg_lo:[0,1]
	v_pk_fma_f32 v[16:17], v[178:179], v[16:17], v[34:35] op_sel_hi:[1,0,1]
	v_pk_mul_f32 v[34:35], v[56:57], v[16:17] op_sel:[1,1] op_sel_hi:[1,0] neg_lo:[1,0]
	v_add_u32_e32 v10, 0x13980, v13
	v_pk_fma_f32 v[34:35], v[56:57], v[16:17], v[34:35] op_sel_hi:[0,1,1]
	ds_write_b64 v10, v[34:35]
	v_pk_mul_f32 v[34:35], v[178:179], v[16:17] op_sel:[1,1] op_sel_hi:[0,1] neg_lo:[0,1]
	v_pk_fma_f32 v[16:17], v[178:179], v[16:17], v[34:35] op_sel_hi:[1,0,1]
	v_pk_mul_f32 v[34:35], v[30:31], v[16:17] op_sel:[1,1] op_sel_hi:[1,0] neg_lo:[1,0]
	v_add_u32_e32 v10, 0x14a00, v13
	v_pk_fma_f32 v[30:31], v[30:31], v[16:17], v[34:35] op_sel_hi:[0,1,1]
	ds_write_b64 v10, v[30:31]
	v_pk_mul_f32 v[30:31], v[178:179], v[16:17] op_sel:[1,1] op_sel_hi:[0,1] neg_lo:[0,1]
	v_pk_fma_f32 v[16:17], v[178:179], v[16:17], v[30:31] op_sel_hi:[1,0,1]
	v_pk_mul_f32 v[30:31], v[50:51], v[16:17] op_sel:[1,1] op_sel_hi:[1,0] neg_lo:[1,0]
	v_add_u32_e32 v10, 0x15a80, v13
	v_pk_fma_f32 v[30:31], v[50:51], v[16:17], v[30:31] op_sel_hi:[0,1,1]
	ds_write_b64 v10, v[30:31]
	v_pk_mul_f32 v[30:31], v[178:179], v[16:17] op_sel:[1,1] op_sel_hi:[0,1] neg_lo:[0,1]
	v_pk_fma_f32 v[16:17], v[178:179], v[16:17], v[30:31] op_sel_hi:[1,0,1]
	v_pk_mul_f32 v[30:31], v[32:33], v[16:17] op_sel:[1,1] op_sel_hi:[1,0] neg_lo:[1,0]
	v_add_u32_e32 v10, 0x16b00, v13
	v_pk_fma_f32 v[30:31], v[32:33], v[16:17], v[30:31] op_sel_hi:[0,1,1]
	ds_write_b64 v10, v[30:31]
	v_pk_mul_f32 v[30:31], v[178:179], v[16:17] op_sel:[1,1] op_sel_hi:[0,1] neg_lo:[0,1]
	v_pk_fma_f32 v[16:17], v[178:179], v[16:17], v[30:31] op_sel_hi:[1,0,1]
	v_pk_mul_f32 v[30:31], v[52:53], v[16:17] op_sel:[1,1] op_sel_hi:[1,0] neg_lo:[1,0]
	v_add_u32_e32 v10, 0x17b80, v13
	v_pk_fma_f32 v[30:31], v[52:53], v[16:17], v[30:31] op_sel_hi:[0,1,1]
	ds_write_b64 v10, v[30:31]
	v_pk_mul_f32 v[30:31], v[178:179], v[16:17] op_sel:[1,1] op_sel_hi:[0,1] neg_lo:[0,1]
	v_pk_fma_f32 v[16:17], v[178:179], v[16:17], v[30:31] op_sel_hi:[1,0,1]
	v_pk_mul_f32 v[30:31], v[24:25], v[16:17] op_sel:[1,1] op_sel_hi:[1,0] neg_lo:[1,0]
	v_add_u32_e32 v10, 0x18c00, v13
	v_pk_fma_f32 v[24:25], v[24:25], v[16:17], v[30:31] op_sel_hi:[0,1,1]
	ds_write_b64 v10, v[24:25]
	v_pk_mul_f32 v[24:25], v[178:179], v[16:17] op_sel:[1,1] op_sel_hi:[0,1] neg_lo:[0,1]
	v_pk_fma_f32 v[16:17], v[178:179], v[16:17], v[24:25] op_sel_hi:[1,0,1]
	v_pk_mul_f32 v[24:25], v[40:41], v[16:17] op_sel:[1,1] op_sel_hi:[1,0] neg_lo:[1,0]
	v_add_u32_e32 v10, 0x19c80, v13
	v_pk_fma_f32 v[24:25], v[40:41], v[16:17], v[24:25] op_sel_hi:[0,1,1]
	ds_write_b64 v10, v[24:25]
	v_pk_mul_f32 v[24:25], v[178:179], v[16:17] op_sel:[1,1] op_sel_hi:[0,1] neg_lo:[0,1]
	v_pk_fma_f32 v[16:17], v[178:179], v[16:17], v[24:25] op_sel_hi:[1,0,1]
	v_pk_mul_f32 v[24:25], v[26:27], v[16:17] op_sel:[1,1] op_sel_hi:[1,0] neg_lo:[1,0]
	v_add_u32_e32 v10, 0x1ad00, v13
	v_pk_fma_f32 v[24:25], v[26:27], v[16:17], v[24:25] op_sel_hi:[0,1,1]
	ds_write_b64 v10, v[24:25]
	v_pk_mul_f32 v[24:25], v[178:179], v[16:17] op_sel:[1,1] op_sel_hi:[0,1] neg_lo:[0,1]
	v_pk_fma_f32 v[16:17], v[178:179], v[16:17], v[24:25] op_sel_hi:[1,0,1]
	v_pk_mul_f32 v[24:25], v[44:45], v[16:17] op_sel:[1,1] op_sel_hi:[1,0] neg_lo:[1,0]
	v_add_u32_e32 v10, 0x1bd80, v13
	v_pk_fma_f32 v[24:25], v[44:45], v[16:17], v[24:25] op_sel_hi:[0,1,1]
	ds_write_b64 v10, v[24:25]
	v_pk_mul_f32 v[24:25], v[178:179], v[16:17] op_sel:[1,1] op_sel_hi:[0,1] neg_lo:[0,1]
	v_pk_fma_f32 v[16:17], v[178:179], v[16:17], v[24:25] op_sel_hi:[1,0,1]
	v_pk_mul_f32 v[24:25], v[20:21], v[16:17] op_sel:[1,1] op_sel_hi:[1,0] neg_lo:[1,0]
	v_add_u32_e32 v10, 0x1ce00, v13
	v_pk_fma_f32 v[20:21], v[20:21], v[16:17], v[24:25] op_sel_hi:[0,1,1]
	ds_write_b64 v10, v[20:21]
	v_pk_mul_f32 v[20:21], v[178:179], v[16:17] op_sel:[1,1] op_sel_hi:[0,1] neg_lo:[0,1]
	v_pk_fma_f32 v[16:17], v[178:179], v[16:17], v[20:21] op_sel_hi:[1,0,1]
	v_pk_mul_f32 v[20:21], v[36:37], v[16:17] op_sel:[1,1] op_sel_hi:[1,0] neg_lo:[1,0]
	v_add_u32_e32 v10, 0x1de80, v13
	v_pk_fma_f32 v[20:21], v[36:37], v[16:17], v[20:21] op_sel_hi:[0,1,1]
	ds_write_b64 v10, v[20:21]
	v_pk_mul_f32 v[20:21], v[178:179], v[16:17] op_sel:[1,1] op_sel_hi:[0,1] neg_lo:[0,1]
	v_pk_fma_f32 v[16:17], v[178:179], v[16:17], v[20:21] op_sel_hi:[1,0,1]
	v_pk_mul_f32 v[20:21], v[22:23], v[16:17] op_sel:[1,1] op_sel_hi:[1,0] neg_lo:[1,0]
	v_add_u32_e32 v10, 0x1ef00, v13
	v_pk_fma_f32 v[20:21], v[22:23], v[16:17], v[20:21] op_sel_hi:[0,1,1]
	ds_write_b64 v10, v[20:21]
	v_pk_mul_f32 v[20:21], v[178:179], v[16:17] op_sel:[1,1] op_sel_hi:[0,1] neg_lo:[0,1]
	v_pk_fma_f32 v[16:17], v[178:179], v[16:17], v[20:21] op_sel_hi:[1,0,1]
	v_pk_mul_f32 v[18:19], v[28:29], v[16:17] op_sel:[1,1] op_sel_hi:[1,0] neg_lo:[1,0]
	v_add_u32_e32 v10, 0x1ff80, v13
	v_pk_fma_f32 v[16:17], v[28:29], v[16:17], v[18:19] op_sel_hi:[0,1,1]
	ds_write_b64 v10, v[16:17]
	v_mov_b32_e32 v10, v174
	v_mov_b32_e32 v13, v172
	s_waitcnt lgkmcnt(0)
	s_barrier
	v_mov_b32_e32 v16, v180
	v_add_u32_e32 v15, v13, v10
	v_lshl_add_u32 v75, v15, 3, 0
	v_xad_u32 v15, v13, 1, v10
	v_lshl_add_u32 v74, v15, 3, 0
	v_xad_u32 v15, v13, 2, v10
	v_lshl_add_u32 v73, v15, 3, 0
	v_xad_u32 v15, v13, 3, v10
	v_lshl_add_u32 v72, v15, 3, 0
	v_xad_u32 v15, v13, 4, v10
	v_lshl_add_u32 v71, v15, 3, 0
	v_xad_u32 v15, v13, 5, v10
	v_lshl_add_u32 v70, v15, 3, 0
	v_xad_u32 v15, v13, 6, v10
	v_lshl_add_u32 v69, v15, 3, 0
	v_xad_u32 v15, v13, 7, v10
	v_lshl_add_u32 v68, v15, 3, 0
	v_xad_u32 v15, v13, 8, v10
	v_lshl_add_u32 v15, v15, 3, 0
	v_add_u32_e32 v67, 0x800, v15
	v_xad_u32 v15, v13, 9, v10
	v_lshl_add_u32 v15, v15, 3, 0
	v_add_u32_e32 v66, 0x800, v15
	v_xad_u32 v15, v13, 10, v10
	v_lshl_add_u32 v15, v15, 3, 0
	v_add_u32_e32 v65, 0x800, v15
	v_xad_u32 v15, v13, 11, v10
	v_lshl_add_u32 v15, v15, 3, 0
	v_add_u32_e32 v64, 0x800, v15
	v_xad_u32 v15, v13, 12, v10
	v_mov_b32_e32 v17, v181
	v_lshl_add_u32 v15, v15, 3, 0
	ds_read2_b64 v[18:21], v75 offset1:16
	ds_read2_b64 v[40:43], v67 offset1:16
	v_add_u32_e32 v63, 0x800, v15
	v_xad_u32 v15, v13, 13, v10
	v_lshl_add_u32 v15, v15, 3, 0
	v_add_u32_e32 v62, 0x800, v15
	v_xad_u32 v15, v13, 14, v10
	v_xad_u32 v10, v13, 15, v10
	ds_read2_b64 v[22:25], v74 offset0:32 offset1:48
	ds_read2_b64 v[48:51], v66 offset0:32 offset1:48
	v_lshl_add_u32 v15, v15, 3, 0
	v_lshl_add_u32 v10, v10, 3, 0
	v_add_u32_e32 v15, 0x800, v15
	v_add_u32_e32 v13, 0x800, v10
	v_mov_b32_e32 v10, v1
	ds_read2_b64 v[26:29], v73 offset0:64 offset1:80
	ds_read2_b64 v[58:61], v72 offset0:96 offset1:112
	ds_read2_b64 v[76:79], v71 offset0:128 offset1:144
	ds_read2_b64 v[80:83], v70 offset0:160 offset1:176
	ds_read2_b64 v[84:87], v69 offset0:192 offset1:208
	ds_read2_b64 v[88:91], v68 offset0:224 offset1:240
	ds_read2_b64 v[54:57], v65 offset0:64 offset1:80
	ds_read2_b64 v[92:95], v64 offset0:96 offset1:112
	ds_read2_b64 v[96:99], v63 offset0:128 offset1:144
	ds_read2_b64 v[100:103], v62 offset0:160 offset1:176
	ds_read2_b64 v[104:107], v15 offset0:192 offset1:208
	ds_read2_b64 v[108:111], v13 offset0:224 offset1:240
	s_waitcnt lgkmcnt(14)
	v_pk_add_f32 v[112:113], v[18:19], v[40:41]
	v_pk_add_f32 v[40:41], v[18:19], v[40:41] neg_lo:[0,1] neg_hi:[0,1]
	v_pk_add_f32 v[18:19], v[20:21], v[42:43]
	v_pk_add_f32 v[20:21], v[20:21], v[42:43] neg_lo:[0,1] neg_hi:[0,1]
	v_mov_b32_e32 v30, v164
	v_mov_b32_e32 v32, v165
	v_mov_b32_e32 v34, v166
	v_mov_b32_e32 v10, v167
	v_mov_b32_e32 v38, v168
	v_mov_b32_e32 v36, v169
	v_mov_b32_e32 v46, v170
	v_mov_b32_e32 v31, v171
	v_pk_mul_f32 v[42:43], v[20:21], v[46:47] op_sel:[1,0] op_sel_hi:[0,0] neg_lo:[1,1] neg_hi:[0,1]
	v_pk_fma_f32 v[44:45], v[20:21], v[30:31], v[42:43] op_sel_hi:[1,0,1]
	s_waitcnt lgkmcnt(12)
	v_pk_add_f32 v[20:21], v[22:23], v[48:49]
	v_pk_add_f32 v[22:23], v[22:23], v[48:49] neg_lo:[0,1] neg_hi:[0,1]
	v_pk_mul_f32 v[42:43], v[22:23], v[36:37] op_sel:[1,0] op_sel_hi:[0,0] neg_lo:[1,1] neg_hi:[0,1]
	v_pk_fma_f32 v[48:49], v[22:23], v[32:33], v[42:43] op_sel_hi:[1,0,1]
	v_pk_add_f32 v[22:23], v[24:25], v[50:51]
	v_pk_add_f32 v[24:25], v[24:25], v[50:51] neg_lo:[0,1] neg_hi:[0,1]
	v_pk_mul_f32 v[42:43], v[24:25], v[38:39] op_sel:[1,0] op_sel_hi:[0,0] neg_lo:[1,1] neg_hi:[0,1]
	v_pk_fma_f32 v[52:53], v[24:25], v[34:35], v[42:43] op_sel_hi:[1,0,1]
	s_waitcnt lgkmcnt(5)
	v_pk_add_f32 v[24:25], v[26:27], v[54:55]
	v_pk_add_f32 v[26:27], v[26:27], v[54:55] neg_lo:[0,1] neg_hi:[0,1]
	v_pk_mul_f32 v[42:43], v[26:27], v[10:11] op_sel:[1,0] op_sel_hi:[0,0] neg_lo:[1,1] neg_hi:[0,1]
	v_pk_fma_f32 v[54:55], v[26:27], v[10:11], v[42:43] op_sel_hi:[1,0,1]
	v_pk_add_f32 v[26:27], v[28:29], v[56:57]
	v_pk_add_f32 v[28:29], v[28:29], v[56:57] neg_lo:[0,1] neg_hi:[0,1]
	v_pk_mul_f32 v[42:43], v[28:29], v[38:39] op_sel_hi:[1,0]
	v_pk_fma_f32 v[56:57], v[28:29], v[34:35], v[42:43] op_sel:[1,0,0] op_sel_hi:[0,0,1] neg_lo:[1,1,0] neg_hi:[0,1,0]
	s_waitcnt lgkmcnt(4)
	v_pk_add_f32 v[42:43], v[58:59], v[92:93] neg_lo:[0,1] neg_hi:[0,1]
	v_pk_add_f32 v[28:29], v[58:59], v[92:93]
	v_pk_mul_f32 v[50:51], v[42:43], v[36:37] op_sel_hi:[1,0]
	v_pk_fma_f32 v[58:59], v[42:43], v[32:33], v[50:51] op_sel:[1,0,0] op_sel_hi:[0,0,1] neg_lo:[1,1,0] neg_hi:[0,1,0]
	v_pk_add_f32 v[50:51], v[60:61], v[94:95] neg_lo:[0,1] neg_hi:[0,1]
	v_pk_add_f32 v[42:43], v[60:61], v[94:95]
	v_pk_mul_f32 v[60:61], v[50:51], v[46:47] op_sel_hi:[1,0]
	v_xor_b32_e32 v92, 0x80000000, v51
	v_mov_b32_e32 v93, v50
	s_waitcnt lgkmcnt(3)
	v_pk_add_f32 v[50:51], v[76:77], v[96:97]
	v_pk_add_f32 v[76:77], v[76:77], v[96:97] neg_lo:[0,1] neg_hi:[0,1]
	v_pk_fma_f32 v[60:61], v[92:93], v[30:31], v[60:61] op_sel_hi:[1,0,1] neg_lo:[0,1,0] neg_hi:[0,1,0]
	v_xor_b32_e32 v93, 0x80000000, v76
	v_mov_b32_e32 v92, v77
	v_pk_add_f32 v[76:77], v[78:79], v[98:99]
	v_pk_add_f32 v[78:79], v[78:79], v[98:99] neg_lo:[0,1] neg_hi:[0,1]
	v_pk_mul_f32 v[94:95], v[78:79], v[46:47] op_sel_hi:[1,0] neg_lo:[0,1] neg_hi:[0,1]
	v_pk_fma_f32 v[78:79], v[78:79], v[30:31], v[94:95] op_sel:[1,0,0] op_sel_hi:[0,0,1] neg_lo:[1,1,0] neg_hi:[0,1,0]
	s_waitcnt lgkmcnt(2)
	v_pk_add_f32 v[94:95], v[80:81], v[100:101]
	v_pk_add_f32 v[80:81], v[80:81], v[100:101] neg_lo:[0,1] neg_hi:[0,1]
	v_pk_mul_f32 v[96:97], v[80:81], v[36:37] op_sel_hi:[1,0] neg_lo:[0,1] neg_hi:[0,1]
	v_pk_fma_f32 v[80:81], v[80:81], v[32:33], v[96:97] op_sel:[1,0,0] op_sel_hi:[0,0,1] neg_lo:[1,1,0] neg_hi:[0,1,0]
	v_pk_add_f32 v[96:97], v[82:83], v[102:103]
	v_pk_add_f32 v[82:83], v[82:83], v[102:103] neg_lo:[0,1] neg_hi:[0,1]
	v_pk_mul_f32 v[98:99], v[82:83], v[38:39] op_sel_hi:[1,0] neg_lo:[0,1] neg_hi:[0,1]
	v_pk_fma_f32 v[82:83], v[82:83], v[34:35], v[98:99] op_sel:[1,0,0] op_sel_hi:[0,0,1] neg_lo:[1,1,0] neg_hi:[0,1,0]
	s_waitcnt lgkmcnt(1)
	v_pk_add_f32 v[98:99], v[84:85], v[104:105]
	v_pk_add_f32 v[84:85], v[84:85], v[104:105] neg_lo:[0,1] neg_hi:[0,1]
	v_pk_mul_f32 v[100:101], v[84:85], v[10:11] op_sel:[1,0] op_sel_hi:[0,0] neg_lo:[1,1] neg_hi:[0,1]
	v_pk_fma_f32 v[84:85], v[84:85], v[10:11], v[100:101] op_sel_hi:[1,0,1] neg_lo:[0,1,0] neg_hi:[0,1,0]
	v_pk_add_f32 v[100:101], v[86:87], v[106:107]
	v_pk_add_f32 v[86:87], v[86:87], v[106:107] neg_lo:[0,1] neg_hi:[0,1]
	v_pk_mul_f32 v[38:39], v[86:87], v[38:39] op_sel:[1,0] op_sel_hi:[0,0] neg_lo:[1,1] neg_hi:[0,1]
	v_pk_fma_f32 v[86:87], v[86:87], v[34:35], v[38:39] op_sel_hi:[1,0,1] neg_lo:[0,1,0] neg_hi:[0,1,0]
	s_waitcnt lgkmcnt(0)
	v_pk_add_f32 v[38:39], v[88:89], v[108:109] neg_lo:[0,1] neg_hi:[0,1]
	v_pk_add_f32 v[34:35], v[88:89], v[108:109]
	v_pk_mul_f32 v[88:89], v[38:39], v[36:37] op_sel:[1,0] op_sel_hi:[0,0] neg_lo:[1,1] neg_hi:[0,1]
	v_pk_fma_f32 v[88:89], v[38:39], v[32:33], v[88:89] op_sel_hi:[1,0,1] neg_lo:[0,1,0] neg_hi:[0,1,0]
	v_pk_add_f32 v[38:39], v[90:91], v[110:111]
	v_pk_add_f32 v[90:91], v[90:91], v[110:111] neg_lo:[0,1] neg_hi:[0,1]
	v_pk_mul_f32 v[46:47], v[90:91], v[46:47] op_sel:[1,0] op_sel_hi:[0,0] neg_lo:[1,1] neg_hi:[0,1]
	v_pk_fma_f32 v[90:91], v[90:91], v[30:31], v[46:47] op_sel_hi:[1,0,1] neg_lo:[0,1,0] neg_hi:[0,1,0]
	v_pk_add_f32 v[46:47], v[18:19], v[76:77]
	v_pk_add_f32 v[18:19], v[18:19], v[76:77] neg_lo:[0,1] neg_hi:[0,1]
	v_pk_add_f32 v[30:31], v[112:113], v[50:51]
	v_pk_mul_f32 v[76:77], v[18:19], v[36:37] op_sel:[1,0] op_sel_hi:[0,0] neg_lo:[1,1] neg_hi:[0,1]
	v_pk_add_f32 v[50:51], v[112:113], v[50:51] neg_lo:[0,1] neg_hi:[0,1]
	v_pk_fma_f32 v[76:77], v[18:19], v[32:33], v[76:77] op_sel_hi:[1,0,1]
	v_pk_add_f32 v[18:19], v[20:21], v[94:95]
	v_pk_add_f32 v[20:21], v[20:21], v[94:95] neg_lo:[0,1] neg_hi:[0,1]
	v_pk_mul_f32 v[94:95], v[20:21], v[10:11] op_sel:[1,0] op_sel_hi:[0,0] neg_lo:[1,1] neg_hi:[0,1]
	v_pk_fma_f32 v[20:21], v[20:21], v[10:11], v[94:95] op_sel_hi:[1,0,1]
	v_pk_add_f32 v[94:95], v[22:23], v[96:97]
	v_pk_add_f32 v[22:23], v[22:23], v[96:97] neg_lo:[0,1] neg_hi:[0,1]
	v_pk_mul_f32 v[96:97], v[22:23], v[36:37] op_sel_hi:[1,0]
	v_xor_b32_e32 v102, 0x80000000, v23
	v_mov_b32_e32 v103, v22
	v_pk_add_f32 v[22:23], v[24:25], v[98:99]
	v_pk_add_f32 v[24:25], v[24:25], v[98:99] neg_lo:[0,1] neg_hi:[0,1]
	v_pk_fma_f32 v[96:97], v[102:103], v[32:33], v[96:97] op_sel_hi:[1,0,1] neg_lo:[0,1,0] neg_hi:[0,1,0]
	v_xor_b32_e32 v99, 0x80000000, v24
	v_mov_b32_e32 v98, v25
	v_pk_add_f32 v[24:25], v[26:27], v[100:101]
	v_pk_add_f32 v[26:27], v[26:27], v[100:101] neg_lo:[0,1] neg_hi:[0,1]
	v_pk_mul_f32 v[100:101], v[26:27], v[36:37] op_sel_hi:[1,0] neg_lo:[0,1] neg_hi:[0,1]
	v_xor_b32_e32 v102, 0x80000000, v27
	v_mov_b32_e32 v103, v26
	v_pk_add_f32 v[26:27], v[28:29], v[34:35]
	v_pk_add_f32 v[28:29], v[28:29], v[34:35] neg_lo:[0,1] neg_hi:[0,1]
	v_pk_fma_f32 v[100:101], v[102:103], v[32:33], v[100:101] op_sel_hi:[1,0,1] neg_lo:[0,1,0] neg_hi:[0,1,0]
	v_pk_mul_f32 v[34:35], v[28:29], v[10:11] op_sel:[1,0] op_sel_hi:[0,0] neg_lo:[1,1] neg_hi:[0,1]
	v_pk_add_f32 v[102:103], v[30:31], v[22:23] neg_lo:[0,1] neg_hi:[0,1]
	v_pk_fma_f32 v[28:29], v[28:29], v[10:11], v[34:35] op_sel_hi:[1,0,1] neg_lo:[0,1,0] neg_hi:[0,1,0]
	v_pk_add_f32 v[34:35], v[42:43], v[38:39]
	v_pk_add_f32 v[38:39], v[42:43], v[38:39] neg_lo:[0,1] neg_hi:[0,1]
	v_pk_mul_f32 v[42:43], v[38:39], v[36:37] op_sel:[1,0] op_sel_hi:[0,0] neg_lo:[1,1] neg_hi:[0,1]
	v_pk_fma_f32 v[42:43], v[38:39], v[32:33], v[42:43] op_sel_hi:[1,0,1] neg_lo:[0,1,0] neg_hi:[0,1,0]
	v_pk_add_f32 v[38:39], v[30:31], v[22:23]
	v_pk_add_f32 v[22:23], v[46:47], v[24:25]
	v_pk_add_f32 v[24:25], v[46:47], v[24:25] neg_lo:[0,1] neg_hi:[0,1]
	v_pk_mul_f32 v[30:31], v[24:25], v[10:11] op_sel:[1,0] op_sel_hi:[0,0] neg_lo:[1,1] neg_hi:[0,1]
	v_pk_fma_f32 v[24:25], v[24:25], v[10:11], v[30:31] op_sel_hi:[1,0,1]
	v_pk_add_f32 v[30:31], v[18:19], v[26:27]
	v_pk_add_f32 v[18:19], v[18:19], v[26:27] neg_lo:[0,1] neg_hi:[0,1]
	v_xor_b32_e32 v27, 0x80000000, v18
	v_mov_b32_e32 v26, v19
	v_pk_add_f32 v[18:19], v[94:95], v[34:35]
	v_pk_add_f32 v[34:35], v[94:95], v[34:35] neg_lo:[0,1] neg_hi:[0,1]
	v_pk_mul_f32 v[46:47], v[34:35], v[10:11] op_sel:[1,0] op_sel_hi:[0,0] neg_lo:[1,1] neg_hi:[0,1]
	v_pk_fma_f32 v[34:35], v[34:35], v[10:11], v[46:47] op_sel_hi:[1,0,1] neg_lo:[0,1,0] neg_hi:[0,1,0]
	v_pk_add_f32 v[46:47], v[38:39], v[30:31]
	v_pk_add_f32 v[38:39], v[38:39], v[30:31] neg_lo:[0,1] neg_hi:[0,1]
	v_pk_add_f32 v[30:31], v[22:23], v[18:19]
	v_pk_add_f32 v[18:19], v[22:23], v[18:19] neg_lo:[0,1] neg_hi:[0,1]
	v_pk_add_f32 v[94:95], v[46:47], v[30:31]
	v_xor_b32_e32 v23, 0x80000000, v18
	v_mov_b32_e32 v22, v19
	v_pk_add_f32 v[18:19], v[102:103], v[26:27]
	v_pk_add_f32 v[102:103], v[102:103], v[26:27] neg_lo:[0,1] neg_hi:[0,1]
	v_pk_add_f32 v[26:27], v[24:25], v[34:35]
	v_pk_add_f32 v[24:25], v[24:25], v[34:35] neg_lo:[0,1] neg_hi:[0,1]
	v_pk_add_f32 v[30:31], v[46:47], v[30:31] neg_lo:[0,1] neg_hi:[0,1]
	v_xor_b32_e32 v35, 0x80000000, v24
	v_mov_b32_e32 v34, v25
	v_pk_add_f32 v[24:25], v[50:51], v[98:99]
	v_pk_add_f32 v[98:99], v[50:51], v[98:99] neg_lo:[0,1] neg_hi:[0,1]
	v_pk_add_f32 v[50:51], v[76:77], v[100:101] neg_lo:[0,1] neg_hi:[0,1]
	v_pk_add_f32 v[46:47], v[38:39], v[22:23]
	v_pk_add_f32 v[22:23], v[38:39], v[22:23] neg_lo:[0,1] neg_hi:[0,1]
	v_pk_add_f32 v[104:105], v[18:19], v[26:27]
	v_pk_add_f32 v[26:27], v[18:19], v[26:27] neg_lo:[0,1] neg_hi:[0,1]
	v_pk_add_f32 v[38:39], v[102:103], v[34:35]
	v_pk_add_f32 v[18:19], v[102:103], v[34:35] neg_lo:[0,1] neg_hi:[0,1]
	v_pk_add_f32 v[34:35], v[76:77], v[100:101]
	v_pk_mul_f32 v[76:77], v[10:11], v[50:51] op_sel:[0,1] op_sel_hi:[0,0] neg_lo:[1,1] neg_hi:[1,0]
	v_pk_fma_f32 v[76:77], v[10:11], v[50:51], v[76:77] op_sel_hi:[0,1,1]
	v_pk_add_f32 v[50:51], v[20:21], v[28:29]
	v_pk_add_f32 v[20:21], v[20:21], v[28:29] neg_lo:[0,1] neg_hi:[0,1]
	v_xor_b32_e32 v29, 0x80000000, v20
	v_mov_b32_e32 v28, v21
	v_pk_add_f32 v[20:21], v[96:97], v[42:43]
	v_pk_add_f32 v[42:43], v[96:97], v[42:43] neg_lo:[0,1] neg_hi:[0,1]
	v_pk_mul_f32 v[96:97], v[10:11], v[42:43] op_sel:[0,1] op_sel_hi:[0,0] neg_lo:[1,1] neg_hi:[1,0]
	v_pk_fma_f32 v[42:43], v[10:11], v[42:43], v[96:97] op_sel_hi:[0,1,1] neg_lo:[1,0,0] neg_hi:[1,0,0]
	v_pk_add_f32 v[96:97], v[24:25], v[50:51]
	v_pk_add_f32 v[24:25], v[24:25], v[50:51] neg_lo:[0,1] neg_hi:[0,1]
	v_pk_add_f32 v[50:51], v[34:35], v[20:21]
	v_pk_add_f32 v[20:21], v[34:35], v[20:21] neg_lo:[0,1] neg_hi:[0,1]
	v_pk_add_f32 v[102:103], v[96:97], v[50:51]
	v_xor_b32_e32 v101, 0x80000000, v20
	v_mov_b32_e32 v100, v21
	v_pk_add_f32 v[34:35], v[96:97], v[50:51] neg_lo:[0,1] neg_hi:[0,1]
	v_pk_add_f32 v[20:21], v[98:99], v[28:29]
	v_pk_add_f32 v[96:97], v[98:99], v[28:29] neg_lo:[0,1] neg_hi:[0,1]
	v_pk_add_f32 v[28:29], v[76:77], v[42:43]
	v_pk_add_f32 v[42:43], v[76:77], v[42:43] neg_lo:[0,1] neg_hi:[0,1]
	v_pk_add_f32 v[98:99], v[20:21], v[28:29]
	v_xor_b32_e32 v77, 0x80000000, v42
	v_mov_b32_e32 v76, v43
	v_pk_add_f32 v[28:29], v[20:21], v[28:29] neg_lo:[0,1] neg_hi:[0,1]
	v_pk_add_f32 v[42:43], v[96:97], v[76:77]
	v_pk_add_f32 v[20:21], v[96:97], v[76:77] neg_lo:[0,1] neg_hi:[0,1]
	v_pk_add_f32 v[76:77], v[40:41], v[92:93]
	v_pk_add_f32 v[92:93], v[40:41], v[92:93] neg_lo:[0,1] neg_hi:[0,1]
	v_pk_add_f32 v[40:41], v[44:45], v[78:79]
	v_pk_add_f32 v[44:45], v[44:45], v[78:79] neg_lo:[0,1] neg_hi:[0,1]
	v_pk_add_f32 v[50:51], v[24:25], v[100:101]
	v_pk_mul_f32 v[78:79], v[36:37], v[44:45] op_sel:[0,1] op_sel_hi:[0,0] neg_lo:[1,1] neg_hi:[1,0]
	v_pk_fma_f32 v[44:45], v[32:33], v[44:45], v[78:79] op_sel_hi:[0,1,1]
	v_pk_add_f32 v[78:79], v[48:49], v[80:81]
	v_pk_add_f32 v[48:49], v[48:49], v[80:81] neg_lo:[0,1] neg_hi:[0,1]
	v_pk_add_f32 v[24:25], v[24:25], v[100:101] neg_lo:[0,1] neg_hi:[0,1]
	v_pk_mul_f32 v[80:81], v[10:11], v[48:49] op_sel:[0,1] op_sel_hi:[0,0] neg_lo:[1,1] neg_hi:[1,0]
	v_pk_fma_f32 v[80:81], v[10:11], v[48:49], v[80:81] op_sel_hi:[0,1,1]
	v_pk_add_f32 v[48:49], v[52:53], v[82:83]
	v_pk_add_f32 v[52:53], v[52:53], v[82:83] neg_lo:[0,1] neg_hi:[0,1]
	v_pk_mul_f32 v[82:83], v[32:33], v[52:53] op_sel:[0,1] op_sel_hi:[0,0] neg_lo:[1,1] neg_hi:[1,0]
	v_pk_fma_f32 v[52:53], v[36:37], v[52:53], v[82:83] op_sel_hi:[0,1,1]
	v_pk_add_f32 v[82:83], v[54:55], v[84:85]
	v_pk_add_f32 v[54:55], v[54:55], v[84:85] neg_lo:[0,1] neg_hi:[0,1]
	v_xor_b32_e32 v85, 0x80000000, v54
	v_mov_b32_e32 v84, v55
	v_pk_add_f32 v[54:55], v[56:57], v[86:87]
	v_pk_add_f32 v[56:57], v[56:57], v[86:87] neg_lo:[0,1] neg_hi:[0,1]
	v_pk_mul_f32 v[86:87], v[32:33], v[56:57] op_sel:[0,1] op_sel_hi:[0,0] neg_lo:[1,1] neg_hi:[1,0]
	v_pk_fma_f32 v[56:57], v[36:37], v[56:57], v[86:87] op_sel_hi:[0,1,1] neg_lo:[1,0,0] neg_hi:[1,0,0]
	v_pk_add_f32 v[86:87], v[58:59], v[88:89]
	v_pk_add_f32 v[58:59], v[58:59], v[88:89] neg_lo:[0,1] neg_hi:[0,1]
	v_pk_mul_f32 v[88:89], v[10:11], v[58:59] op_sel:[0,1] op_sel_hi:[0,0] neg_lo:[1,1] neg_hi:[1,0]
	v_pk_fma_f32 v[58:59], v[10:11], v[58:59], v[88:89] op_sel_hi:[0,1,1] neg_lo:[1,0,0] neg_hi:[1,0,0]
	v_pk_add_f32 v[88:89], v[60:61], v[90:91]
	v_pk_add_f32 v[60:61], v[60:61], v[90:91] neg_lo:[0,1] neg_hi:[0,1]
	v_pk_mul_f32 v[36:37], v[36:37], v[60:61] op_sel:[0,1] op_sel_hi:[0,0] neg_lo:[1,1] neg_hi:[1,0]
	v_pk_fma_f32 v[36:37], v[32:33], v[60:61], v[36:37] op_sel_hi:[0,1,1] neg_lo:[1,0,0] neg_hi:[1,0,0]
	v_pk_add_f32 v[32:33], v[76:77], v[82:83]
	v_pk_add_f32 v[60:61], v[76:77], v[82:83] neg_lo:[0,1] neg_hi:[0,1]
	v_pk_add_f32 v[76:77], v[54:55], v[40:41]
	v_pk_add_f32 v[40:41], v[40:41], v[54:55] neg_lo:[0,1] neg_hi:[0,1]
	v_pk_mul_f32 v[54:55], v[10:11], v[40:41] op_sel:[0,1] op_sel_hi:[0,0] neg_lo:[1,1] neg_hi:[1,0]
	v_pk_fma_f32 v[54:55], v[10:11], v[40:41], v[54:55] op_sel_hi:[0,1,1]
	v_pk_add_f32 v[40:41], v[78:79], v[86:87]
	v_pk_add_f32 v[78:79], v[78:79], v[86:87] neg_lo:[0,1] neg_hi:[0,1]
	v_xor_b32_e32 v83, 0x80000000, v78
	v_mov_b32_e32 v82, v79
	v_pk_add_f32 v[78:79], v[48:49], v[88:89]
	v_pk_add_f32 v[48:49], v[48:49], v[88:89] neg_lo:[0,1] neg_hi:[0,1]
	v_pk_add_f32 v[88:89], v[76:77], v[78:79]
	v_pk_mul_f32 v[86:87], v[10:11], v[48:49] op_sel:[0,1] op_sel_hi:[0,0] neg_lo:[1,1] neg_hi:[1,0]
	v_pk_fma_f32 v[48:49], v[10:11], v[48:49], v[86:87] op_sel_hi:[0,1,1] neg_lo:[1,0,0] neg_hi:[1,0,0]
	v_pk_add_f32 v[86:87], v[32:33], v[40:41]
	v_pk_add_f32 v[32:33], v[32:33], v[40:41] neg_lo:[0,1] neg_hi:[0,1]
	v_pk_add_f32 v[40:41], v[76:77], v[78:79] neg_lo:[0,1] neg_hi:[0,1]
	v_pk_add_f32 v[78:79], v[86:87], v[88:89] neg_lo:[0,1] neg_hi:[0,1]
	v_pk_add_f32 v[90:91], v[32:33], v[40:41] op_sel:[0,1] op_sel_hi:[1,0] neg_hi:[0,1]
	v_pk_add_f32 v[40:41], v[32:33], v[40:41] op_sel:[0,1] op_sel_hi:[1,0] neg_lo:[0,1]
	v_pk_add_f32 v[76:77], v[54:55], v[48:49]
	v_pk_add_f32 v[48:49], v[54:55], v[48:49] neg_lo:[0,1] neg_hi:[0,1]
	v_pk_add_f32 v[32:33], v[60:61], v[82:83]
	v_pk_add_f32 v[60:61], v[60:61], v[82:83] neg_lo:[0,1] neg_hi:[0,1]
	v_xor_b32_e32 v55, 0x80000000, v48
	v_mov_b32_e32 v54, v49
	v_pk_add_f32 v[82:83], v[32:33], v[76:77]
	v_pk_add_f32 v[48:49], v[32:33], v[76:77] neg_lo:[0,1] neg_hi:[0,1]
	v_pk_add_f32 v[76:77], v[60:61], v[54:55]
	v_pk_add_f32 v[32:33], v[60:61], v[54:55] neg_lo:[0,1] neg_hi:[0,1]
	v_pk_add_f32 v[54:55], v[92:93], v[84:85]
	v_pk_add_f32 v[60:61], v[92:93], v[84:85] neg_lo:[0,1] neg_hi:[0,1]
	v_pk_add_f32 v[84:85], v[56:57], v[44:45]
	v_pk_add_f32 v[44:45], v[44:45], v[56:57] neg_lo:[0,1] neg_hi:[0,1]
	v_pk_add_f32 v[86:87], v[86:87], v[88:89]
	v_pk_mul_f32 v[56:57], v[10:11], v[44:45] op_sel:[0,1] op_sel_hi:[0,0] neg_lo:[1,1] neg_hi:[1,0]
	v_pk_fma_f32 v[56:57], v[10:11], v[44:45], v[56:57] op_sel_hi:[0,1,1]
	v_pk_add_f32 v[44:45], v[80:81], v[58:59]
	v_pk_add_f32 v[58:59], v[80:81], v[58:59] neg_lo:[0,1] neg_hi:[0,1]
	v_xor_b32_e32 v81, 0x80000000, v58
	v_mov_b32_e32 v80, v59
	v_pk_add_f32 v[58:59], v[52:53], v[36:37]
	v_pk_add_f32 v[36:37], v[52:53], v[36:37] neg_lo:[0,1] neg_hi:[0,1]
	v_pk_mul_f32 v[52:53], v[10:11], v[36:37] op_sel:[0,1] op_sel_hi:[0,0] neg_lo:[1,1] neg_hi:[1,0]
	v_pk_fma_f32 v[36:37], v[10:11], v[36:37], v[52:53] op_sel_hi:[0,1,1] neg_lo:[1,0,0] neg_hi:[1,0,0]
	v_pk_add_f32 v[52:53], v[54:55], v[44:45]
	v_pk_add_f32 v[44:45], v[54:55], v[44:45] neg_lo:[0,1] neg_hi:[0,1]
	v_pk_add_f32 v[54:55], v[84:85], v[58:59]
	v_pk_add_f32 v[58:59], v[84:85], v[58:59] neg_lo:[0,1] neg_hi:[0,1]
	v_xor_b32_e32 v85, 0x80000000, v58
	v_mov_b32_e32 v84, v59
	v_pk_add_f32 v[58:59], v[52:53], v[54:55]
	v_pk_add_f32 v[52:53], v[52:53], v[54:55] neg_lo:[0,1] neg_hi:[0,1]
	v_pk_add_f32 v[54:55], v[44:45], v[84:85]
	v_pk_add_f32 v[44:45], v[44:45], v[84:85] neg_lo:[0,1] neg_hi:[0,1]
	v_pk_add_f32 v[84:85], v[60:61], v[80:81]
	v_pk_add_f32 v[60:61], v[60:61], v[80:81] neg_lo:[0,1] neg_hi:[0,1]
	v_pk_add_f32 v[80:81], v[56:57], v[36:37]
	v_pk_add_f32 v[36:37], v[56:57], v[36:37] neg_lo:[0,1] neg_hi:[0,1]
	v_pk_add_f32 v[92:93], v[84:85], v[80:81]
	v_pk_add_f32 v[80:81], v[84:85], v[80:81] neg_lo:[0,1] neg_hi:[0,1]
	v_pk_add_f32 v[84:85], v[60:61], v[36:37] op_sel:[0,1] op_sel_hi:[1,0] neg_hi:[0,1]
	v_pk_add_f32 v[36:37], v[60:61], v[36:37] op_sel:[0,1] op_sel_hi:[1,0] neg_lo:[0,1]
	v_pk_fma_f32 v[60:61], v[16:17], s[90:91], v[16:17] op_sel:[1,0,0] op_sel_hi:[0,1,1]
	v_pk_mul_f32 v[56:57], v[94:95], s[14:15] op_sel:[1,0] neg_lo:[1,0]
	v_pk_mul_f32 v[88:89], v[60:61], v[86:87] op_sel:[1,1] op_sel_hi:[0,1] neg_lo:[0,1]
	v_pk_fma_f32 v[56:57], v[94:95], s[94:95], v[56:57] op_sel_hi:[0,1,1]
	v_pk_fma_f32 v[86:87], v[60:61], v[86:87], v[88:89] op_sel_hi:[1,0,1]
	ds_write2_b64 v75, v[56:57], v[86:87] offset1:16
	v_pk_mul_f32 v[56:57], v[16:17], v[60:61] op_sel:[1,1] op_sel_hi:[0,1] neg_lo:[0,1]
	v_pk_fma_f32 v[56:57], v[16:17], v[60:61], v[56:57] op_sel_hi:[1,0,1]
	v_pk_mul_f32 v[60:61], v[56:57], v[102:103] op_sel:[1,1] op_sel_hi:[0,1] neg_lo:[0,1]
	v_pk_mul_f32 v[86:87], v[16:17], v[56:57] op_sel:[1,1] op_sel_hi:[0,1] neg_lo:[0,1]
	v_pk_fma_f32 v[60:61], v[56:57], v[102:103], v[60:61] op_sel_hi:[1,0,1]
	v_pk_fma_f32 v[56:57], v[16:17], v[56:57], v[86:87] op_sel_hi:[1,0,1]
	v_pk_mul_f32 v[86:87], v[56:57], v[58:59] op_sel:[1,1] op_sel_hi:[0,1] neg_lo:[0,1]
	v_pk_fma_f32 v[58:59], v[56:57], v[58:59], v[86:87] op_sel_hi:[1,0,1]
	ds_write2_b64 v74, v[60:61], v[58:59] offset0:32 offset1:48
	v_pk_mul_f32 v[58:59], v[16:17], v[56:57] op_sel:[1,1] op_sel_hi:[0,1] neg_lo:[0,1]
	v_pk_fma_f32 v[56:57], v[16:17], v[56:57], v[58:59] op_sel_hi:[1,0,1]
	v_pk_mul_f32 v[58:59], v[56:57], v[104:105] op_sel:[1,1] op_sel_hi:[0,1] neg_lo:[0,1]
	v_pk_mul_f32 v[60:61], v[16:17], v[56:57] op_sel:[1,1] op_sel_hi:[0,1] neg_lo:[0,1]
	v_pk_fma_f32 v[58:59], v[56:57], v[104:105], v[58:59] op_sel_hi:[1,0,1]
	v_pk_fma_f32 v[56:57], v[16:17], v[56:57], v[60:61] op_sel_hi:[1,0,1]
	v_pk_mul_f32 v[60:61], v[56:57], v[82:83] op_sel:[1,1] op_sel_hi:[0,1] neg_lo:[0,1]
	v_pk_fma_f32 v[60:61], v[56:57], v[82:83], v[60:61] op_sel_hi:[1,0,1]
	ds_write2_b64 v73, v[58:59], v[60:61] offset0:64 offset1:80
	v_pk_mul_f32 v[58:59], v[16:17], v[56:57] op_sel:[1,1] op_sel_hi:[0,1] neg_lo:[0,1]
	v_pk_fma_f32 v[56:57], v[16:17], v[56:57], v[58:59] op_sel_hi:[1,0,1]
	v_pk_mul_f32 v[58:59], v[56:57], v[98:99] op_sel:[1,1] op_sel_hi:[0,1] neg_lo:[0,1]
	v_pk_mul_f32 v[60:61], v[16:17], v[56:57] op_sel:[1,1] op_sel_hi:[0,1] neg_lo:[0,1]
	v_pk_fma_f32 v[58:59], v[56:57], v[98:99], v[58:59] op_sel_hi:[1,0,1]
	v_pk_fma_f32 v[56:57], v[16:17], v[56:57], v[60:61] op_sel_hi:[1,0,1]
	v_pk_mul_f32 v[60:61], v[56:57], v[92:93] op_sel:[1,1] op_sel_hi:[0,1] neg_lo:[0,1]
	v_pk_fma_f32 v[60:61], v[56:57], v[92:93], v[60:61] op_sel_hi:[1,0,1]
	ds_write2_b64 v72, v[58:59], v[60:61] offset0:96 offset1:112
	v_pk_mul_f32 v[58:59], v[16:17], v[56:57] op_sel:[1,1] op_sel_hi:[0,1] neg_lo:[0,1]
	v_pk_fma_f32 v[56:57], v[16:17], v[56:57], v[58:59] op_sel_hi:[1,0,1]
	v_pk_mul_f32 v[58:59], v[56:57], v[46:47] op_sel:[1,1] op_sel_hi:[0,1] neg_lo:[0,1]
	v_pk_fma_f32 v[46:47], v[56:57], v[46:47], v[58:59] op_sel_hi:[1,0,1]
	v_pk_mul_f32 v[58:59], v[16:17], v[56:57] op_sel:[1,1] op_sel_hi:[0,1] neg_lo:[0,1]
	v_pk_fma_f32 v[56:57], v[16:17], v[56:57], v[58:59] op_sel_hi:[1,0,1]
	v_pk_mul_f32 v[58:59], v[56:57], v[90:91] op_sel:[1,1] op_sel_hi:[0,1] neg_lo:[0,1]
	v_pk_fma_f32 v[58:59], v[56:57], v[90:91], v[58:59] op_sel_hi:[1,0,1]
	ds_write2_b64 v71, v[46:47], v[58:59] offset0:128 offset1:144
	v_pk_mul_f32 v[46:47], v[16:17], v[56:57] op_sel:[1,1] op_sel_hi:[0,1] neg_lo:[0,1]
	v_pk_fma_f32 v[46:47], v[16:17], v[56:57], v[46:47] op_sel_hi:[1,0,1]
	v_pk_mul_f32 v[56:57], v[46:47], v[50:51] op_sel:[1,1] op_sel_hi:[0,1] neg_lo:[0,1]
	v_pk_fma_f32 v[50:51], v[46:47], v[50:51], v[56:57] op_sel_hi:[1,0,1]
	v_pk_mul_f32 v[56:57], v[16:17], v[46:47] op_sel:[1,1] op_sel_hi:[0,1] neg_lo:[0,1]
	v_pk_fma_f32 v[46:47], v[16:17], v[46:47], v[56:57] op_sel_hi:[1,0,1]
	v_pk_mul_f32 v[56:57], v[46:47], v[54:55] op_sel:[1,1] op_sel_hi:[0,1] neg_lo:[0,1]
	v_pk_fma_f32 v[54:55], v[46:47], v[54:55], v[56:57] op_sel_hi:[1,0,1]
	ds_write2_b64 v70, v[50:51], v[54:55] offset0:160 offset1:176
	v_pk_mul_f32 v[50:51], v[16:17], v[46:47] op_sel:[1,1] op_sel_hi:[0,1] neg_lo:[0,1]
	v_pk_fma_f32 v[46:47], v[16:17], v[46:47], v[50:51] op_sel_hi:[1,0,1]
	v_pk_mul_f32 v[50:51], v[38:39], v[46:47] op_sel:[1,1] op_sel_hi:[1,0] neg_lo:[1,0]
	v_pk_fma_f32 v[38:39], v[38:39], v[46:47], v[50:51] op_sel_hi:[0,1,1]
	v_pk_mul_f32 v[50:51], v[16:17], v[46:47] op_sel:[1,1] op_sel_hi:[0,1] neg_lo:[0,1]
	v_pk_fma_f32 v[46:47], v[16:17], v[46:47], v[50:51] op_sel_hi:[1,0,1]
	v_pk_mul_f32 v[50:51], v[46:47], v[76:77] op_sel:[1,1] op_sel_hi:[0,1] neg_lo:[0,1]
	v_pk_fma_f32 v[50:51], v[46:47], v[76:77], v[50:51] op_sel_hi:[1,0,1]
	ds_write2_b64 v69, v[38:39], v[50:51] offset0:192 offset1:208
	v_pk_mul_f32 v[38:39], v[16:17], v[46:47] op_sel:[1,1] op_sel_hi:[0,1] neg_lo:[0,1]
	v_pk_fma_f32 v[38:39], v[16:17], v[46:47], v[38:39] op_sel_hi:[1,0,1]
	v_pk_mul_f32 v[46:47], v[42:43], v[38:39] op_sel:[1,1] op_sel_hi:[1,0] neg_lo:[1,0]
	v_pk_fma_f32 v[42:43], v[42:43], v[38:39], v[46:47] op_sel_hi:[0,1,1]
	v_pk_mul_f32 v[46:47], v[16:17], v[38:39] op_sel:[1,1] op_sel_hi:[0,1] neg_lo:[0,1]
	v_pk_fma_f32 v[38:39], v[16:17], v[38:39], v[46:47] op_sel_hi:[1,0,1]
	v_pk_mul_f32 v[46:47], v[38:39], v[84:85] op_sel:[1,1] op_sel_hi:[0,1] neg_lo:[0,1]
	v_pk_fma_f32 v[46:47], v[38:39], v[84:85], v[46:47] op_sel_hi:[1,0,1]
	ds_write2_b64 v68, v[42:43], v[46:47] offset0:224 offset1:240
	v_pk_mul_f32 v[42:43], v[16:17], v[38:39] op_sel:[1,1] op_sel_hi:[0,1] neg_lo:[0,1]
	v_pk_fma_f32 v[38:39], v[16:17], v[38:39], v[42:43] op_sel_hi:[1,0,1]
	v_pk_mul_f32 v[42:43], v[30:31], v[38:39] op_sel:[1,1] op_sel_hi:[1,0] neg_lo:[1,0]
	v_pk_fma_f32 v[30:31], v[30:31], v[38:39], v[42:43] op_sel_hi:[0,1,1]
	v_pk_mul_f32 v[42:43], v[16:17], v[38:39] op_sel:[1,1] op_sel_hi:[0,1] neg_lo:[0,1]
	v_pk_fma_f32 v[38:39], v[16:17], v[38:39], v[42:43] op_sel_hi:[1,0,1]
	v_pk_mul_f32 v[42:43], v[78:79], v[38:39] op_sel:[1,1] op_sel_hi:[1,0] neg_lo:[1,0]
	v_pk_fma_f32 v[42:43], v[78:79], v[38:39], v[42:43] op_sel_hi:[0,1,1]
	ds_write2_b64 v67, v[30:31], v[42:43] offset1:16
	v_pk_mul_f32 v[30:31], v[16:17], v[38:39] op_sel:[1,1] op_sel_hi:[0,1] neg_lo:[0,1]
	v_pk_fma_f32 v[30:31], v[16:17], v[38:39], v[30:31] op_sel_hi:[1,0,1]
	v_pk_mul_f32 v[38:39], v[34:35], v[30:31] op_sel:[1,1] op_sel_hi:[1,0] neg_lo:[1,0]
	v_pk_fma_f32 v[34:35], v[34:35], v[30:31], v[38:39] op_sel_hi:[0,1,1]
	v_pk_mul_f32 v[38:39], v[16:17], v[30:31] op_sel:[1,1] op_sel_hi:[0,1] neg_lo:[0,1]
	v_pk_fma_f32 v[30:31], v[16:17], v[30:31], v[38:39] op_sel_hi:[1,0,1]
	v_pk_mul_f32 v[38:39], v[52:53], v[30:31] op_sel:[1,1] op_sel_hi:[1,0] neg_lo:[1,0]
	v_pk_fma_f32 v[38:39], v[52:53], v[30:31], v[38:39] op_sel_hi:[0,1,1]
	ds_write2_b64 v66, v[34:35], v[38:39] offset0:32 offset1:48
	v_pk_mul_f32 v[34:35], v[16:17], v[30:31] op_sel:[1,1] op_sel_hi:[0,1] neg_lo:[0,1]
	v_pk_fma_f32 v[30:31], v[16:17], v[30:31], v[34:35] op_sel_hi:[1,0,1]
	v_pk_mul_f32 v[34:35], v[26:27], v[30:31] op_sel:[1,1] op_sel_hi:[1,0] neg_lo:[1,0]
	v_pk_fma_f32 v[26:27], v[26:27], v[30:31], v[34:35] op_sel_hi:[0,1,1]
	v_pk_mul_f32 v[34:35], v[16:17], v[30:31] op_sel:[1,1] op_sel_hi:[0,1] neg_lo:[0,1]
	v_pk_fma_f32 v[30:31], v[16:17], v[30:31], v[34:35] op_sel_hi:[1,0,1]
	v_pk_mul_f32 v[34:35], v[48:49], v[30:31] op_sel:[1,1] op_sel_hi:[1,0] neg_lo:[1,0]
	v_pk_fma_f32 v[34:35], v[48:49], v[30:31], v[34:35] op_sel_hi:[0,1,1]
	ds_write2_b64 v65, v[26:27], v[34:35] offset0:64 offset1:80
	v_pk_mul_f32 v[26:27], v[16:17], v[30:31] op_sel:[1,1] op_sel_hi:[0,1] neg_lo:[0,1]
	v_pk_fma_f32 v[26:27], v[16:17], v[30:31], v[26:27] op_sel_hi:[1,0,1]
	v_pk_mul_f32 v[30:31], v[28:29], v[26:27] op_sel:[1,1] op_sel_hi:[1,0] neg_lo:[1,0]
	v_pk_fma_f32 v[28:29], v[28:29], v[26:27], v[30:31] op_sel_hi:[0,1,1]
	v_pk_mul_f32 v[30:31], v[16:17], v[26:27] op_sel:[1,1] op_sel_hi:[0,1] neg_lo:[0,1]
	v_pk_fma_f32 v[26:27], v[16:17], v[26:27], v[30:31] op_sel_hi:[1,0,1]
	v_pk_mul_f32 v[30:31], v[80:81], v[26:27] op_sel:[1,1] op_sel_hi:[1,0] neg_lo:[1,0]
	v_pk_fma_f32 v[30:31], v[80:81], v[26:27], v[30:31] op_sel_hi:[0,1,1]
	ds_write2_b64 v64, v[28:29], v[30:31] offset0:96 offset1:112
	v_pk_mul_f32 v[28:29], v[16:17], v[26:27] op_sel:[1,1] op_sel_hi:[0,1] neg_lo:[0,1]
	v_pk_fma_f32 v[26:27], v[16:17], v[26:27], v[28:29] op_sel_hi:[1,0,1]
	v_pk_mul_f32 v[28:29], v[22:23], v[26:27] op_sel:[1,1] op_sel_hi:[1,0] neg_lo:[1,0]
	v_pk_fma_f32 v[22:23], v[22:23], v[26:27], v[28:29] op_sel_hi:[0,1,1]
	v_pk_mul_f32 v[28:29], v[16:17], v[26:27] op_sel:[1,1] op_sel_hi:[0,1] neg_lo:[0,1]
	v_pk_fma_f32 v[26:27], v[16:17], v[26:27], v[28:29] op_sel_hi:[1,0,1]
	v_pk_mul_f32 v[28:29], v[40:41], v[26:27] op_sel:[1,1] op_sel_hi:[1,0] neg_lo:[1,0]
	v_pk_fma_f32 v[28:29], v[40:41], v[26:27], v[28:29] op_sel_hi:[0,1,1]
	ds_write2_b64 v63, v[22:23], v[28:29] offset0:128 offset1:144
	v_pk_mul_f32 v[22:23], v[16:17], v[26:27] op_sel:[1,1] op_sel_hi:[0,1] neg_lo:[0,1]
	v_pk_fma_f32 v[22:23], v[16:17], v[26:27], v[22:23] op_sel_hi:[1,0,1]
	v_pk_mul_f32 v[26:27], v[24:25], v[22:23] op_sel:[1,1] op_sel_hi:[1,0] neg_lo:[1,0]
	v_pk_fma_f32 v[24:25], v[24:25], v[22:23], v[26:27] op_sel_hi:[0,1,1]
	v_pk_mul_f32 v[26:27], v[16:17], v[22:23] op_sel:[1,1] op_sel_hi:[0,1] neg_lo:[0,1]
	v_pk_fma_f32 v[22:23], v[16:17], v[22:23], v[26:27] op_sel_hi:[1,0,1]
	v_pk_mul_f32 v[26:27], v[44:45], v[22:23] op_sel:[1,1] op_sel_hi:[1,0] neg_lo:[1,0]
	v_pk_fma_f32 v[26:27], v[44:45], v[22:23], v[26:27] op_sel_hi:[0,1,1]
	ds_write2_b64 v62, v[24:25], v[26:27] offset0:160 offset1:176
	v_pk_mul_f32 v[24:25], v[16:17], v[22:23] op_sel:[1,1] op_sel_hi:[0,1] neg_lo:[0,1]
	v_pk_fma_f32 v[22:23], v[16:17], v[22:23], v[24:25] op_sel_hi:[1,0,1]
	v_pk_mul_f32 v[24:25], v[18:19], v[22:23] op_sel:[1,1] op_sel_hi:[1,0] neg_lo:[1,0]
	v_pk_fma_f32 v[18:19], v[18:19], v[22:23], v[24:25] op_sel_hi:[0,1,1]
	v_pk_mul_f32 v[24:25], v[16:17], v[22:23] op_sel:[1,1] op_sel_hi:[0,1] neg_lo:[0,1]
	v_pk_fma_f32 v[22:23], v[16:17], v[22:23], v[24:25] op_sel_hi:[1,0,1]
	v_pk_mul_f32 v[24:25], v[32:33], v[22:23] op_sel:[1,1] op_sel_hi:[1,0] neg_lo:[1,0]
	v_pk_fma_f32 v[24:25], v[32:33], v[22:23], v[24:25] op_sel_hi:[0,1,1]
	ds_write2_b64 v15, v[18:19], v[24:25] offset0:192 offset1:208
	v_pk_mul_f32 v[18:19], v[16:17], v[22:23] op_sel:[1,1] op_sel_hi:[0,1] neg_lo:[0,1]
	v_pk_fma_f32 v[18:19], v[16:17], v[22:23], v[18:19] op_sel_hi:[1,0,1]
	v_pk_mul_f32 v[22:23], v[20:21], v[18:19] op_sel:[1,1] op_sel_hi:[1,0] neg_lo:[1,0]
	v_pk_fma_f32 v[20:21], v[20:21], v[18:19], v[22:23] op_sel_hi:[0,1,1]
	v_pk_mul_f32 v[22:23], v[16:17], v[18:19] op_sel:[1,1] op_sel_hi:[0,1] neg_lo:[0,1]
	v_pk_fma_f32 v[16:17], v[16:17], v[18:19], v[22:23] op_sel_hi:[1,0,1]
	v_pk_mul_f32 v[18:19], v[36:37], v[16:17] op_sel:[1,1] op_sel_hi:[1,0] neg_lo:[1,0]
	v_pk_fma_f32 v[16:17], v[36:37], v[16:17], v[18:19] op_sel_hi:[0,1,1]
	ds_write2_b64 v13, v[20:21], v[16:17] offset0:224 offset1:240
	v_mov_b32_e32 v16, v182
	v_mov_b32_e32 v10, v176
	v_mov_b32_e32 v17, v175
	s_waitcnt lgkmcnt(0)
	s_barrier
	v_lshlrev_b32_e32 v190, 3, v16
	v_add_u32_e32 v190, 0x1000, v190
	global_load_dwordx2 v[202:203], v190, s[46:47] offset:-4096
	global_load_dwordx2 v[204:205], v190, s[46:47]
	v_add_u32_e32 v190, 0x2000, v190
	global_load_dwordx2 v[206:207], v190, s[46:47] offset:-4096
	global_load_dwordx2 v[208:209], v190, s[46:47]
	v_add_u32_e32 v190, 0x2000, v190
	global_load_dwordx2 v[210:211], v190, s[46:47] offset:-4096
	global_load_dwordx2 v[212:213], v190, s[46:47]
	v_add_u32_e32 v190, 0x2000, v190
	global_load_dwordx2 v[214:215], v190, s[46:47] offset:-4096
	global_load_dwordx2 v[216:217], v190, s[46:47]
	v_add_u32_e32 v190, 0x2000, v190
	global_load_dwordx2 v[218:219], v190, s[46:47] offset:-4096
	global_load_dwordx2 v[220:221], v190, s[46:47]
	v_add_u32_e32 v190, 0x2000, v190
	global_load_dwordx2 v[222:223], v190, s[46:47] offset:-4096
	global_load_dwordx2 v[224:225], v190, s[46:47]
	v_add_u32_e32 v190, 0x2000, v190
	global_load_dwordx2 v[226:227], v190, s[46:47] offset:-4096
	global_load_dwordx2 v[228:229], v190, s[46:47]
	v_add_u32_e32 v190, 0x2000, v190
	global_load_dwordx2 v[230:231], v190, s[46:47] offset:-4096
	global_load_dwordx2 v[232:233], v190, s[46:47]
	v_mov_b32_e32 v50, v165
	v_lshlrev_b32_e32 v13, 3, v17
	v_lshlrev_b32_e32 v48, 3, v10
	v_add3_u32 v10, 0, v13, v48
	v_xor_b32_e32 v13, 1, v17
	v_xor_b32_e32 v34, 8, v17
	v_xor_b32_e32 v36, 9, v17
	v_lshlrev_b32_e32 v13, 3, v13
	v_xor_b32_e32 v15, 2, v17
	v_xor_b32_e32 v24, 3, v17
	v_xor_b32_e32 v26, 4, v17
	v_xor_b32_e32 v28, 5, v17
	v_xor_b32_e32 v30, 6, v17
	v_xor_b32_e32 v32, 7, v17
	v_lshlrev_b32_e32 v34, 3, v34
	v_lshlrev_b32_e32 v36, 3, v36
	v_xor_b32_e32 v38, 10, v17
	v_xor_b32_e32 v40, 11, v17
	v_xor_b32_e32 v42, 12, v17
	v_xor_b32_e32 v44, 13, v17
	v_xor_b32_e32 v46, 14, v17
	v_xor_b32_e32 v17, 15, v17
	v_add3_u32 v13, 0, v13, v48
	v_lshlrev_b32_e32 v15, 3, v15
	v_lshlrev_b32_e32 v24, 3, v24
	v_lshlrev_b32_e32 v26, 3, v26
	v_lshlrev_b32_e32 v28, 3, v28
	v_lshlrev_b32_e32 v30, 3, v30
	v_lshlrev_b32_e32 v32, 3, v32
	v_add3_u32 v57, 0, v34, v48
	v_add3_u32 v58, 0, v36, v48
	v_lshlrev_b32_e32 v38, 3, v38
	v_lshlrev_b32_e32 v40, 3, v40
	v_lshlrev_b32_e32 v42, 3, v42
	v_lshlrev_b32_e32 v44, 3, v44
	v_lshlrev_b32_e32 v46, 3, v46
	v_lshlrev_b32_e32 v17, 3, v17
	ds_read_b64 v[18:19], v10
	ds_read_b64 v[20:21], v13
	v_add3_u32 v15, 0, v15, v48
	v_add3_u32 v52, 0, v24, v48
	v_add3_u32 v53, 0, v26, v48
	v_add3_u32 v54, 0, v28, v48
	v_add3_u32 v55, 0, v30, v48
	v_add3_u32 v56, 0, v32, v48
	ds_read_b64 v[34:35], v57
	ds_read_b64 v[36:37], v58
	v_add3_u32 v59, 0, v38, v48
	v_add3_u32 v60, 0, v40, v48
	v_add3_u32 v61, 0, v42, v48
	v_add3_u32 v62, 0, v44, v48
	v_add3_u32 v63, 0, v46, v48
	v_add3_u32 v64, 0, v17, v48
	v_mov_b32_e32 v17, v1
	ds_read_b64 v[22:23], v15
	ds_read_b64 v[24:25], v52
	ds_read_b64 v[26:27], v53
	ds_read_b64 v[28:29], v54
	ds_read_b64 v[30:31], v55
	ds_read_b64 v[32:33], v56
	ds_read_b64 v[38:39], v59
	ds_read_b64 v[40:41], v60
	ds_read_b64 v[42:43], v61
	ds_read_b64 v[44:45], v62
	ds_read_b64 v[46:47], v63
	ds_read_b64 v[48:49], v64
	s_waitcnt lgkmcnt(13)
	v_pk_add_f32 v[70:71], v[18:19], v[34:35]
	v_mov_b32_e32 v17, v164
	v_pk_add_f32 v[18:19], v[18:19], v[34:35] neg_lo:[0,1] neg_hi:[0,1]
	v_mov_b32_e32 v17, v166
	s_waitcnt lgkmcnt(12)
	v_pk_add_f32 v[34:35], v[20:21], v[36:37]
	v_pk_add_f32 v[20:21], v[20:21], v[36:37] neg_lo:[0,1] neg_hi:[0,1]
	v_mov_b32_e32 v66, v167
	v_mov_b32_e32 v17, v168
	v_mov_b32_e32 v68, v169
	s_nop 0
	v_pk_mul_f32 v[36:37], v[20:21], v[68:69] op_sel:[1,0] op_sel_hi:[0,0] neg_lo:[1,1] neg_hi:[0,1]
	v_mov_b32_e32 v17, v170
	v_pk_fma_f32 v[20:21], v[20:21], v[50:51], v[36:37] op_sel_hi:[1,0,1]
	s_waitcnt lgkmcnt(5)
	v_pk_add_f32 v[36:37], v[22:23], v[38:39]
	v_pk_add_f32 v[22:23], v[22:23], v[38:39] neg_lo:[0,1] neg_hi:[0,1]
	v_pk_mul_f32 v[38:39], v[22:23], v[66:67] op_sel:[1,0] op_sel_hi:[0,0] neg_lo:[1,1] neg_hi:[0,1]
	v_mov_b32_e32 v17, v171
	v_pk_fma_f32 v[22:23], v[22:23], v[66:67], v[38:39] op_sel_hi:[1,0,1]
	s_waitcnt lgkmcnt(4)
	v_pk_add_f32 v[38:39], v[24:25], v[40:41]
	v_pk_add_f32 v[24:25], v[24:25], v[40:41] neg_lo:[0,1] neg_hi:[0,1]
	v_pk_mul_f32 v[40:41], v[24:25], v[68:69] op_sel_hi:[1,0]
	v_pk_fma_f32 v[24:25], v[24:25], v[50:51], v[40:41] op_sel:[1,0,0] op_sel_hi:[0,0,1] neg_lo:[1,1,0] neg_hi:[0,1,0]
	s_waitcnt lgkmcnt(3)
	v_pk_add_f32 v[40:41], v[26:27], v[42:43]
	v_pk_add_f32 v[26:27], v[26:27], v[42:43] neg_lo:[0,1] neg_hi:[0,1]
	v_ashrrev_i32_e32 v17, 31, v16
	v_xor_b32_e32 v73, 0x80000000, v26
	v_mov_b32_e32 v72, v27
	s_waitcnt lgkmcnt(2)
	v_pk_add_f32 v[26:27], v[28:29], v[44:45]
	v_pk_add_f32 v[28:29], v[28:29], v[44:45] neg_lo:[0,1] neg_hi:[0,1]
	v_pk_mul_f32 v[42:43], v[28:29], v[68:69] op_sel_hi:[1,0] neg_lo:[0,1] neg_hi:[0,1]
	v_pk_fma_f32 v[28:29], v[28:29], v[50:51], v[42:43] op_sel:[1,0,0] op_sel_hi:[0,0,1] neg_lo:[1,1,0] neg_hi:[0,1,0]
	s_waitcnt lgkmcnt(1)
	v_pk_add_f32 v[42:43], v[30:31], v[46:47]
	v_pk_add_f32 v[30:31], v[30:31], v[46:47] neg_lo:[0,1] neg_hi:[0,1]
	v_pk_mul_f32 v[44:45], v[30:31], v[66:67] op_sel:[1,0] op_sel_hi:[0,0] neg_lo:[1,1] neg_hi:[0,1]
	v_pk_fma_f32 v[30:31], v[30:31], v[66:67], v[44:45] op_sel_hi:[1,0,1] neg_lo:[0,1,0] neg_hi:[0,1,0]
	s_waitcnt lgkmcnt(0)
	v_pk_add_f32 v[44:45], v[32:33], v[48:49]
	v_pk_add_f32 v[32:33], v[32:33], v[48:49] neg_lo:[0,1] neg_hi:[0,1]
	v_pk_add_f32 v[48:49], v[34:35], v[26:27]
	v_pk_add_f32 v[26:27], v[34:35], v[26:27] neg_lo:[0,1] neg_hi:[0,1]
	v_pk_mul_f32 v[34:35], v[26:27], v[66:67] op_sel:[1,0] op_sel_hi:[0,0] neg_lo:[1,1] neg_hi:[0,1]
	v_pk_fma_f32 v[26:27], v[26:27], v[66:67], v[34:35] op_sel_hi:[1,0,1]
	v_pk_add_f32 v[34:35], v[36:37], v[42:43]
	v_pk_add_f32 v[36:37], v[36:37], v[42:43] neg_lo:[0,1] neg_hi:[0,1]
	v_pk_mul_f32 v[46:47], v[32:33], v[68:69] op_sel:[1,0] op_sel_hi:[0,0] neg_lo:[1,1] neg_hi:[0,1]
	v_xor_b32_e32 v43, 0x80000000, v36
	v_mov_b32_e32 v42, v37
	v_pk_add_f32 v[36:37], v[38:39], v[44:45]
	v_pk_add_f32 v[38:39], v[38:39], v[44:45] neg_lo:[0,1] neg_hi:[0,1]
	v_pk_fma_f32 v[46:47], v[32:33], v[50:51], v[46:47] op_sel_hi:[1,0,1] neg_lo:[0,1,0] neg_hi:[0,1,0]
	v_pk_add_f32 v[32:33], v[70:71], v[40:41]
	v_pk_mul_f32 v[44:45], v[38:39], v[66:67] op_sel:[1,0] op_sel_hi:[0,0] neg_lo:[1,1] neg_hi:[0,1]
	v_pk_add_f32 v[40:41], v[70:71], v[40:41] neg_lo:[0,1] neg_hi:[0,1]
	v_pk_fma_f32 v[38:39], v[38:39], v[66:67], v[44:45] op_sel_hi:[1,0,1] neg_lo:[0,1,0] neg_hi:[0,1,0]
	v_pk_add_f32 v[44:45], v[32:33], v[34:35]
	v_pk_add_f32 v[32:33], v[32:33], v[34:35] neg_lo:[0,1] neg_hi:[0,1]
	v_pk_add_f32 v[34:35], v[48:49], v[36:37]
	v_pk_add_f32 v[36:37], v[48:49], v[36:37] neg_lo:[0,1] neg_hi:[0,1]
	v_pk_add_f32 v[50:51], v[44:45], v[34:35]
	v_xor_b32_e32 v49, 0x80000000, v36
	v_mov_b32_e32 v48, v37
	v_pk_add_f32 v[36:37], v[44:45], v[34:35] neg_lo:[0,1] neg_hi:[0,1]
	v_pk_add_f32 v[68:69], v[32:33], v[48:49]
	v_pk_add_f32 v[44:45], v[32:33], v[48:49] neg_lo:[0,1] neg_hi:[0,1]
	v_pk_add_f32 v[32:33], v[40:41], v[42:43]
	v_pk_add_f32 v[34:35], v[40:41], v[42:43] neg_lo:[0,1] neg_hi:[0,1]
	v_pk_add_f32 v[40:41], v[26:27], v[38:39]
	v_pk_add_f32 v[26:27], v[26:27], v[38:39] neg_lo:[0,1] neg_hi:[0,1]
	v_pk_add_f32 v[42:43], v[32:33], v[40:41] neg_lo:[0,1] neg_hi:[0,1]
	v_xor_b32_e32 v39, 0x80000000, v26
	v_mov_b32_e32 v38, v27
	v_pk_add_f32 v[26:27], v[32:33], v[40:41]
	v_pk_add_f32 v[40:41], v[20:21], v[28:29]
	v_pk_add_f32 v[20:21], v[20:21], v[28:29] neg_lo:[0,1] neg_hi:[0,1]
	v_pk_add_f32 v[32:33], v[34:35], v[38:39]
	v_pk_mul_f32 v[28:29], v[66:67], v[20:21] op_sel:[0,1] op_sel_hi:[0,0] neg_lo:[1,1] neg_hi:[1,0]
	v_pk_fma_f32 v[20:21], v[66:67], v[20:21], v[28:29] op_sel_hi:[0,1,1]
	v_pk_add_f32 v[28:29], v[22:23], v[30:31]
	v_pk_add_f32 v[22:23], v[22:23], v[30:31] neg_lo:[0,1] neg_hi:[0,1]
	v_pk_add_f32 v[38:39], v[34:35], v[38:39] neg_lo:[0,1] neg_hi:[0,1]
	v_xor_b32_e32 v31, 0x80000000, v22
	v_mov_b32_e32 v30, v23
	v_pk_add_f32 v[22:23], v[24:25], v[46:47]
	v_pk_add_f32 v[24:25], v[24:25], v[46:47] neg_lo:[0,1] neg_hi:[0,1]
	v_pk_add_f32 v[34:35], v[18:19], v[72:73]
	v_pk_mul_f32 v[46:47], v[66:67], v[24:25] op_sel:[0,1] op_sel_hi:[0,0] neg_lo:[1,1] neg_hi:[1,0]
	v_pk_fma_f32 v[24:25], v[66:67], v[24:25], v[46:47] op_sel_hi:[0,1,1] neg_lo:[1,0,0] neg_hi:[1,0,0]
	v_pk_add_f32 v[46:47], v[34:35], v[28:29]
	v_pk_add_f32 v[28:29], v[34:35], v[28:29] neg_lo:[0,1] neg_hi:[0,1]
	v_pk_add_f32 v[34:35], v[40:41], v[22:23]
	v_pk_add_f32 v[22:23], v[40:41], v[22:23] neg_lo:[0,1] neg_hi:[0,1]
	v_pk_add_f32 v[18:19], v[18:19], v[72:73] neg_lo:[0,1] neg_hi:[0,1]
	v_pk_add_f32 v[66:67], v[28:29], v[22:23] op_sel:[0,1] op_sel_hi:[1,0] neg_hi:[0,1]
	v_pk_add_f32 v[48:49], v[28:29], v[22:23] op_sel:[0,1] op_sel_hi:[1,0] neg_lo:[0,1]
	v_pk_add_f32 v[28:29], v[18:19], v[30:31]
	v_pk_add_f32 v[18:19], v[18:19], v[30:31] neg_lo:[0,1] neg_hi:[0,1]
	v_pk_add_f32 v[30:31], v[20:21], v[24:25]
	v_pk_add_f32 v[20:21], v[20:21], v[24:25] neg_lo:[0,1] neg_hi:[0,1]
	v_pk_add_f32 v[22:23], v[46:47], v[34:35]
	v_xor_b32_e32 v25, 0x80000000, v20
	v_mov_b32_e32 v24, v21
	v_lshl_add_u64 v[20:21], v[16:17], 3, s[46:47]
	s_waitcnt vmcnt(0)
	v_pk_add_f32 v[40:41], v[46:47], v[34:35] neg_lo:[0,1] neg_hi:[0,1]
	v_pk_add_f32 v[34:35], v[18:19], v[24:25]
	v_pk_add_f32 v[18:19], v[18:19], v[24:25] neg_lo:[0,1] neg_hi:[0,1]
	v_pk_add_f32 v[70:71], v[28:29], v[30:31]
	v_pk_add_f32 v[46:47], v[28:29], v[30:31] neg_lo:[0,1] neg_hi:[0,1]
	v_mov_b32_e32 v17, v1
	s_nop 0
	v_pk_mul_f32 v[24:25], v[50:51], v[202:203] op_sel:[1,1] op_sel_hi:[1,0] neg_lo:[1,0]
	v_pk_fma_f32 v[20:21], v[50:51], v[202:203], v[24:25] op_sel_hi:[0,1,1]
	v_add_u32_e32 v24, 0x200, v16
	v_ashrrev_i32_e32 v25, 31, v24
	v_lshl_add_u64 v[24:25], v[24:25], 3, s[46:47]
	s_nop 0
	v_pk_mul_f32 v[28:29], v[204:205], v[22:23] op_sel:[1,1] op_sel_hi:[0,1] neg_lo:[0,1]
	v_pk_fma_f32 v[22:23], v[204:205], v[22:23], v[28:29] op_sel_hi:[1,0,1]
	v_add_u32_e32 v24, 0x400, v16
	v_ashrrev_i32_e32 v25, 31, v24
	v_lshl_add_u64 v[24:25], v[24:25], 3, s[46:47]
	s_nop 0
	v_pk_mul_f32 v[28:29], v[26:27], v[206:207] op_sel:[1,1] op_sel_hi:[1,0] neg_lo:[1,0]
	v_pk_fma_f32 v[24:25], v[26:27], v[206:207], v[28:29] op_sel_hi:[0,1,1]
	v_add_u32_e32 v26, 0x600, v16
	v_ashrrev_i32_e32 v27, 31, v26
	v_lshl_add_u64 v[26:27], v[26:27], 3, s[46:47]
	s_nop 0
	v_pk_mul_f32 v[28:29], v[208:209], v[70:71] op_sel:[1,1] op_sel_hi:[0,1] neg_lo:[0,1]
	v_pk_fma_f32 v[26:27], v[208:209], v[70:71], v[28:29] op_sel_hi:[1,0,1]
	v_add_u32_e32 v28, 0x800, v16
	v_ashrrev_i32_e32 v29, 31, v28
	v_lshl_add_u64 v[28:29], v[28:29], 3, s[46:47]
	s_nop 0
	v_pk_mul_f32 v[30:31], v[68:69], v[210:211] op_sel:[1,1] op_sel_hi:[1,0] neg_lo:[1,0]
	v_pk_fma_f32 v[28:29], v[68:69], v[210:211], v[30:31] op_sel_hi:[0,1,1]
	v_add_u32_e32 v30, 0xa00, v16
	v_ashrrev_i32_e32 v31, 31, v30
	v_lshl_add_u64 v[30:31], v[30:31], 3, s[46:47]
	v_mov_b32_e32 v68, v169
	s_nop 0
	v_pk_mul_f32 v[50:51], v[212:213], v[66:67] op_sel:[1,1] op_sel_hi:[0,1] neg_lo:[0,1]
	v_pk_fma_f32 v[30:31], v[212:213], v[66:67], v[50:51] op_sel_hi:[1,0,1]
	v_add_u32_e32 v50, 0xc00, v16
	v_ashrrev_i32_e32 v51, 31, v50
	v_lshl_add_u64 v[50:51], v[50:51], 3, s[46:47]
	s_nop 0
	v_pk_mul_f32 v[66:67], v[32:33], v[214:215] op_sel:[1,1] op_sel_hi:[1,0] neg_lo:[1,0]
	v_pk_fma_f32 v[32:33], v[32:33], v[214:215], v[66:67] op_sel_hi:[0,1,1]
	v_add_u32_e32 v50, 0xe00, v16
	v_ashrrev_i32_e32 v51, 31, v50
	v_lshl_add_u64 v[50:51], v[50:51], 3, s[46:47]
	s_nop 0
	v_pk_mul_f32 v[66:67], v[216:217], v[34:35] op_sel:[1,1] op_sel_hi:[0,1] neg_lo:[0,1]
	v_pk_fma_f32 v[34:35], v[216:217], v[34:35], v[66:67] op_sel_hi:[1,0,1]
	v_add_u32_e32 v50, 0x1000, v16
	v_ashrrev_i32_e32 v51, 31, v50
	v_lshl_add_u64 v[50:51], v[50:51], 3, s[46:47]
	s_nop 0
	v_pk_mul_f32 v[66:67], v[36:37], v[218:219] op_sel:[1,1] op_sel_hi:[1,0] neg_lo:[1,0]
	v_pk_fma_f32 v[36:37], v[36:37], v[218:219], v[66:67] op_sel_hi:[0,1,1]
	v_add_u32_e32 v50, 0x1200, v16
	v_ashrrev_i32_e32 v51, 31, v50
	v_lshl_add_u64 v[50:51], v[50:51], 3, s[46:47]
	v_pk_add_f32 v[70:71], v[20:21], v[36:37]
	v_pk_add_f32 v[20:21], v[20:21], v[36:37] neg_lo:[0,1] neg_hi:[0,1]
	s_nop 0
	v_pk_mul_f32 v[66:67], v[40:41], v[220:221] op_sel:[1,1] op_sel_hi:[1,0] neg_lo:[1,0]
	v_pk_fma_f32 v[40:41], v[40:41], v[220:221], v[66:67] op_sel_hi:[0,1,1]
	v_add_u32_e32 v50, 0x1400, v16
	v_ashrrev_i32_e32 v51, 31, v50
	v_lshl_add_u64 v[50:51], v[50:51], 3, s[46:47]
	v_pk_add_f32 v[36:37], v[22:23], v[40:41]
	v_pk_add_f32 v[22:23], v[22:23], v[40:41] neg_lo:[0,1] neg_hi:[0,1]
	s_nop 0
	v_pk_mul_f32 v[66:67], v[42:43], v[222:223] op_sel:[1,1] op_sel_hi:[1,0] neg_lo:[1,0]
	v_pk_fma_f32 v[42:43], v[42:43], v[222:223], v[66:67] op_sel_hi:[0,1,1]
	v_add_u32_e32 v50, 0x1600, v16
	v_ashrrev_i32_e32 v51, 31, v50
	v_lshl_add_u64 v[50:51], v[50:51], 3, s[46:47]
	s_nop 0
	v_pk_mul_f32 v[66:67], v[46:47], v[224:225] op_sel:[1,1] op_sel_hi:[1,0] neg_lo:[1,0]
	v_pk_fma_f32 v[46:47], v[46:47], v[224:225], v[66:67] op_sel_hi:[0,1,1]
	v_add_u32_e32 v50, 0x1800, v16
	v_ashrrev_i32_e32 v51, 31, v50
	v_lshl_add_u64 v[50:51], v[50:51], 3, s[46:47]
	s_nop 0
	v_pk_mul_f32 v[66:67], v[44:45], v[226:227] op_sel:[1,1] op_sel_hi:[1,0] neg_lo:[1,0]
	v_pk_fma_f32 v[44:45], v[44:45], v[226:227], v[66:67] op_sel_hi:[0,1,1]
	v_add_u32_e32 v50, 0x1a00, v16
	v_ashrrev_i32_e32 v51, 31, v50
	v_lshl_add_u64 v[50:51], v[50:51], 3, s[46:47]
	s_nop 0
	v_pk_mul_f32 v[66:67], v[48:49], v[228:229] op_sel:[1,1] op_sel_hi:[1,0] neg_lo:[1,0]
	v_pk_fma_f32 v[48:49], v[48:49], v[228:229], v[66:67] op_sel_hi:[0,1,1]
	v_add_u32_e32 v50, 0x1c00, v16
	v_ashrrev_i32_e32 v51, 31, v50
	v_lshl_add_u64 v[50:51], v[50:51], 3, s[46:47]
	s_nop 0
	v_pk_mul_f32 v[66:67], v[38:39], v[230:231] op_sel:[1,1] op_sel_hi:[1,0] neg_lo:[1,0]
	v_pk_fma_f32 v[38:39], v[38:39], v[230:231], v[66:67] op_sel_hi:[0,1,1]
	v_add_u32_e32 v50, 0x1e00, v16
	v_ashrrev_i32_e32 v51, 31, v50
	v_lshl_add_u64 v[50:51], v[50:51], 3, s[46:47]
	v_mov_b32_e32 v50, v232
	v_mov_b32_e32 v51, v233
	v_lshlrev_b32_e32 v190, 3, v16
	v_add_u32_e32 v190, 0x11000, v190
	global_load_dwordx2 v[202:203], v190, s[46:47] offset:-4096
	global_load_dwordx2 v[204:205], v190, s[46:47]
	v_add_u32_e32 v190, 0x2000, v190
	global_load_dwordx2 v[206:207], v190, s[46:47] offset:-4096
	global_load_dwordx2 v[208:209], v190, s[46:47]
	v_add_u32_e32 v190, 0x2000, v190
	global_load_dwordx2 v[210:211], v190, s[46:47] offset:-4096
	global_load_dwordx2 v[212:213], v190, s[46:47]
	v_add_u32_e32 v190, 0x2000, v190
	global_load_dwordx2 v[214:215], v190, s[46:47] offset:-4096
	global_load_dwordx2 v[216:217], v190, s[46:47]
	v_add_u32_e32 v190, 0x2000, v190
	global_load_dwordx2 v[218:219], v190, s[46:47] offset:-4096
	global_load_dwordx2 v[220:221], v190, s[46:47]
	v_add_u32_e32 v190, 0x2000, v190
	global_load_dwordx2 v[222:223], v190, s[46:47] offset:-4096
	global_load_dwordx2 v[224:225], v190, s[46:47]
	v_add_u32_e32 v190, 0x2000, v190
	global_load_dwordx2 v[226:227], v190, s[46:47] offset:-4096
	global_load_dwordx2 v[228:229], v190, s[46:47]
	v_add_u32_e32 v190, 0x2000, v190
	global_load_dwordx2 v[230:231], v190, s[46:47] offset:-4096
	global_load_dwordx2 v[232:233], v190, s[46:47]
	v_mov_b32_e32 v17, v164
	s_nop 0
	v_pk_mul_f32 v[66:67], v[18:19], v[50:51] op_sel:[1,1] op_sel_hi:[1,0] neg_lo:[1,0]
	v_pk_fma_f32 v[18:19], v[18:19], v[50:51], v[66:67] op_sel_hi:[0,1,1]
	v_mov_b32_e32 v50, v165
	v_mov_b32_e32 v17, v166
	v_mov_b32_e32 v66, v167
	v_mov_b32_e32 v17, v168
	s_nop 0
	v_pk_mul_f32 v[40:41], v[22:23], v[68:69] op_sel:[1,0] op_sel_hi:[0,0] neg_lo:[1,0]
	v_mov_b32_e32 v17, v170
	v_pk_fma_f32 v[22:23], v[22:23], v[50:51], v[40:41] op_sel_hi:[1,0,1]
	v_pk_add_f32 v[40:41], v[24:25], v[42:43]
	v_pk_add_f32 v[24:25], v[24:25], v[42:43] neg_lo:[0,1] neg_hi:[0,1]
	v_pk_mul_f32 v[42:43], v[24:25], v[66:67] op_sel:[1,0] op_sel_hi:[0,0] neg_lo:[1,0]
	v_mov_b32_e32 v17, v171
	v_pk_fma_f32 v[24:25], v[24:25], v[66:67], v[42:43] op_sel_hi:[1,0,1]
	v_pk_add_f32 v[42:43], v[26:27], v[46:47]
	v_pk_add_f32 v[26:27], v[26:27], v[46:47] neg_lo:[0,1] neg_hi:[0,1]
	v_pk_mul_f32 v[46:47], v[26:27], v[68:69] op_sel_hi:[1,0]
	v_pk_fma_f32 v[26:27], v[26:27], v[50:51], v[46:47] op_sel:[1,0,0] op_sel_hi:[0,0,1] neg_lo:[1,0,0]
	v_pk_add_f32 v[46:47], v[28:29], v[44:45]
	v_pk_add_f32 v[28:29], v[28:29], v[44:45] neg_lo:[0,1] neg_hi:[0,1]
	v_mov_b32_e32 v17, v175
	v_xor_b32_e32 v44, 0x80000000, v29
	v_mov_b32_e32 v45, v28
	v_pk_add_f32 v[28:29], v[30:31], v[48:49]
	v_pk_add_f32 v[30:31], v[30:31], v[48:49] neg_lo:[0,1] neg_hi:[0,1]
	v_pk_mul_f32 v[48:49], v[30:31], v[68:69] op_sel_hi:[1,0] neg_lo:[0,1] neg_hi:[0,1]
	v_pk_fma_f32 v[30:31], v[30:31], v[50:51], v[48:49] op_sel:[1,0,0] op_sel_hi:[0,0,1] neg_lo:[1,0,0]
	v_pk_add_f32 v[48:49], v[32:33], v[38:39]
	v_pk_add_f32 v[32:33], v[32:33], v[38:39] neg_lo:[0,1] neg_hi:[0,1]
	v_pk_mul_f32 v[38:39], v[32:33], v[66:67] op_sel:[1,0] op_sel_hi:[0,0] neg_lo:[1,0]
	v_pk_fma_f32 v[32:33], v[32:33], v[66:67], v[38:39] op_sel_hi:[1,0,1] neg_lo:[0,1,0] neg_hi:[0,1,0]
	v_pk_add_f32 v[38:39], v[34:35], v[18:19]
	v_pk_add_f32 v[18:19], v[34:35], v[18:19] neg_lo:[0,1] neg_hi:[0,1]
	v_pk_mul_f32 v[34:35], v[18:19], v[68:69] op_sel:[1,0] op_sel_hi:[0,0] neg_lo:[1,0]
	v_mov_b32_e32 v68, v169
	v_pk_fma_f32 v[18:19], v[18:19], v[50:51], v[34:35] op_sel_hi:[1,0,1] neg_lo:[0,1,0] neg_hi:[0,1,0]
	v_pk_add_f32 v[50:51], v[36:37], v[28:29]
	v_pk_add_f32 v[28:29], v[36:37], v[28:29] neg_lo:[0,1] neg_hi:[0,1]
	v_pk_add_f32 v[34:35], v[70:71], v[46:47]
	v_pk_mul_f32 v[36:37], v[28:29], v[66:67] op_sel:[1,0] op_sel_hi:[0,0] neg_lo:[1,0]
	v_pk_add_f32 v[46:47], v[70:71], v[46:47] neg_lo:[0,1] neg_hi:[0,1]
	v_pk_fma_f32 v[28:29], v[28:29], v[66:67], v[36:37] op_sel_hi:[1,0,1]
	v_pk_add_f32 v[36:37], v[40:41], v[48:49]
	v_pk_add_f32 v[40:41], v[40:41], v[48:49] neg_lo:[0,1] neg_hi:[0,1]
	v_xor_b32_e32 v48, 0x80000000, v41
	v_mov_b32_e32 v49, v40
	v_pk_add_f32 v[40:41], v[42:43], v[38:39]
	v_pk_add_f32 v[38:39], v[42:43], v[38:39] neg_lo:[0,1] neg_hi:[0,1]
	v_pk_mul_f32 v[42:43], v[66:67], v[38:39] op_sel:[0,1] op_sel_hi:[0,0] neg_lo:[0,1]
	v_pk_fma_f32 v[38:39], v[38:39], v[66:67], v[42:43] op_sel_hi:[1,0,1] neg_lo:[0,1,0] neg_hi:[0,1,0]
	v_pk_add_f32 v[42:43], v[34:35], v[36:37]
	v_pk_add_f32 v[34:35], v[34:35], v[36:37] neg_lo:[0,1] neg_hi:[0,1]
	v_pk_add_f32 v[36:37], v[50:51], v[40:41]
	v_pk_add_f32 v[40:41], v[50:51], v[40:41] neg_lo:[0,1] neg_hi:[0,1]
	v_xor_b32_e32 v50, 0x80000000, v41
	v_mov_b32_e32 v51, v40
	v_pk_add_f32 v[40:41], v[42:43], v[36:37]
	v_pk_add_f32 v[36:37], v[42:43], v[36:37] neg_lo:[0,1] neg_hi:[0,1]
	v_pk_add_f32 v[42:43], v[34:35], v[50:51]
	v_pk_add_f32 v[34:35], v[34:35], v[50:51] neg_lo:[0,1] neg_hi:[0,1]
	v_pk_add_f32 v[50:51], v[46:47], v[48:49]
	v_pk_add_f32 v[46:47], v[46:47], v[48:49] neg_lo:[0,1] neg_hi:[0,1]
	v_pk_add_f32 v[48:49], v[28:29], v[38:39]
	v_pk_add_f32 v[28:29], v[28:29], v[38:39] neg_lo:[0,1] neg_hi:[0,1]
	v_xor_b32_e32 v38, 0x80000000, v29
	v_mov_b32_e32 v39, v28
	v_pk_add_f32 v[28:29], v[50:51], v[48:49]
	v_pk_add_f32 v[48:49], v[50:51], v[48:49] neg_lo:[0,1] neg_hi:[0,1]
	v_pk_add_f32 v[50:51], v[46:47], v[38:39]
	v_pk_add_f32 v[38:39], v[46:47], v[38:39] neg_lo:[0,1] neg_hi:[0,1]
	v_pk_add_f32 v[46:47], v[20:21], v[44:45]
	v_pk_add_f32 v[20:21], v[20:21], v[44:45] neg_lo:[0,1] neg_hi:[0,1]
	v_pk_add_f32 v[44:45], v[22:23], v[30:31]
	v_pk_add_f32 v[22:23], v[22:23], v[30:31] neg_lo:[0,1] neg_hi:[0,1]
	v_pk_mul_f32 v[30:31], v[66:67], v[22:23] op_sel:[0,1] op_sel_hi:[0,0] neg_lo:[0,1]
	v_pk_fma_f32 v[22:23], v[66:67], v[22:23], v[30:31] op_sel_hi:[0,1,1]
	v_pk_add_f32 v[30:31], v[24:25], v[32:33]
	v_pk_add_f32 v[24:25], v[24:25], v[32:33] neg_lo:[0,1] neg_hi:[0,1]
	v_xor_b32_e32 v32, 0x80000000, v25
	v_mov_b32_e32 v33, v24
	v_pk_add_f32 v[24:25], v[26:27], v[18:19]
	v_pk_add_f32 v[18:19], v[26:27], v[18:19] neg_lo:[0,1] neg_hi:[0,1]
	v_pk_mul_f32 v[26:27], v[66:67], v[18:19] op_sel:[0,1] op_sel_hi:[0,0] neg_lo:[0,1]
	v_pk_fma_f32 v[18:19], v[66:67], v[18:19], v[26:27] op_sel_hi:[0,1,1] neg_lo:[1,0,0] neg_hi:[1,0,0]
	v_pk_add_f32 v[26:27], v[46:47], v[30:31]
	v_pk_add_f32 v[30:31], v[46:47], v[30:31] neg_lo:[0,1] neg_hi:[0,1]
	v_pk_add_f32 v[46:47], v[44:45], v[24:25]
	v_pk_add_f32 v[24:25], v[44:45], v[24:25] neg_lo:[0,1] neg_hi:[0,1]
	v_mov_b32_e32 v66, v167
	v_xor_b32_e32 v44, 0x80000000, v25
	v_mov_b32_e32 v45, v24
	v_pk_add_f32 v[24:25], v[26:27], v[46:47]
	v_pk_add_f32 v[26:27], v[26:27], v[46:47] neg_lo:[0,1] neg_hi:[0,1]
	v_pk_add_f32 v[46:47], v[30:31], v[44:45]
	v_pk_add_f32 v[30:31], v[30:31], v[44:45] neg_lo:[0,1] neg_hi:[0,1]
	v_pk_add_f32 v[44:45], v[20:21], v[32:33]
	v_pk_add_f32 v[20:21], v[20:21], v[32:33] neg_lo:[0,1] neg_hi:[0,1]
	v_pk_add_f32 v[32:33], v[22:23], v[18:19]
	v_pk_add_f32 v[18:19], v[22:23], v[18:19] neg_lo:[0,1] neg_hi:[0,1]
	v_xor_b32_e32 v22, 0x80000000, v19
	v_mov_b32_e32 v23, v18
	v_pk_add_f32 v[18:19], v[44:45], v[32:33]
	v_pk_add_f32 v[32:33], v[44:45], v[32:33] neg_lo:[0,1] neg_hi:[0,1]
	v_pk_add_f32 v[44:45], v[20:21], v[22:23]
	v_pk_add_f32 v[20:21], v[20:21], v[22:23] neg_lo:[0,1] neg_hi:[0,1]
	ds_write_b64 v10, v[40:41]
	ds_write_b64 v13, v[24:25]
	ds_write_b64 v15, v[28:29]
	ds_write_b64 v52, v[18:19]
	ds_write_b64 v53, v[42:43]
	ds_write_b64 v54, v[46:47]
	ds_write_b64 v55, v[50:51]
	ds_write_b64 v56, v[44:45]
	ds_write_b64 v57, v[36:37]
	ds_write_b64 v58, v[26:27]
	ds_write_b64 v59, v[48:49]
	ds_write_b64 v60, v[32:33]
	ds_write_b64 v61, v[34:35]
	ds_write_b64 v62, v[30:31]
	ds_write_b64 v63, v[38:39]
	ds_write_b64 v64, v[20:21]
	v_mov_b32_e32 v10, v177
	v_mov_b32_e32 v64, v165
	v_lshlrev_b32_e32 v13, 3, v17
	v_lshlrev_b32_e32 v48, 3, v10
	v_add3_u32 v10, 0, v13, v48
	v_xor_b32_e32 v13, 1, v17
	v_xor_b32_e32 v34, 8, v17
	v_xor_b32_e32 v36, 9, v17
	v_lshlrev_b32_e32 v13, 3, v13
	v_xor_b32_e32 v15, 2, v17
	v_xor_b32_e32 v24, 3, v17
	v_xor_b32_e32 v26, 4, v17
	v_xor_b32_e32 v28, 5, v17
	v_xor_b32_e32 v30, 6, v17
	v_xor_b32_e32 v32, 7, v17
	v_lshlrev_b32_e32 v34, 3, v34
	v_lshlrev_b32_e32 v36, 3, v36
	v_xor_b32_e32 v38, 10, v17
	v_xor_b32_e32 v40, 11, v17
	v_xor_b32_e32 v42, 12, v17
	v_xor_b32_e32 v44, 13, v17
	v_xor_b32_e32 v46, 14, v17
	v_xor_b32_e32 v17, 15, v17
	v_add3_u32 v13, 0, v13, v48
	v_lshlrev_b32_e32 v15, 3, v15
	v_lshlrev_b32_e32 v24, 3, v24
	v_lshlrev_b32_e32 v26, 3, v26
	v_lshlrev_b32_e32 v28, 3, v28
	v_lshlrev_b32_e32 v30, 3, v30
	v_lshlrev_b32_e32 v32, 3, v32
	v_add3_u32 v55, 0, v34, v48
	v_add3_u32 v56, 0, v36, v48
	v_lshlrev_b32_e32 v38, 3, v38
	v_lshlrev_b32_e32 v40, 3, v40
	v_lshlrev_b32_e32 v42, 3, v42
	v_lshlrev_b32_e32 v44, 3, v44
	v_lshlrev_b32_e32 v46, 3, v46
	v_lshlrev_b32_e32 v17, 3, v17
	ds_read_b64 v[18:19], v10
	ds_read_b64 v[20:21], v13
	v_add3_u32 v15, 0, v15, v48
	v_add3_u32 v50, 0, v24, v48
	v_add3_u32 v51, 0, v26, v48
	v_add3_u32 v52, 0, v28, v48
	v_add3_u32 v53, 0, v30, v48
	v_add3_u32 v54, 0, v32, v48
	ds_read_b64 v[34:35], v55
	ds_read_b64 v[36:37], v56
	v_add3_u32 v57, 0, v38, v48
	v_add3_u32 v58, 0, v40, v48
	v_add3_u32 v59, 0, v42, v48
	v_add3_u32 v60, 0, v44, v48
	v_add3_u32 v61, 0, v46, v48
	v_add3_u32 v62, 0, v17, v48
	v_mov_b32_e32 v17, v1
	ds_read_b64 v[22:23], v15
	ds_read_b64 v[24:25], v50
	ds_read_b64 v[26:27], v51
	ds_read_b64 v[28:29], v52
	ds_read_b64 v[30:31], v53
	ds_read_b64 v[32:33], v54
	ds_read_b64 v[38:39], v57
	ds_read_b64 v[40:41], v58
	ds_read_b64 v[42:43], v59
	ds_read_b64 v[44:45], v60
	ds_read_b64 v[46:47], v61
	ds_read_b64 v[48:49], v62
	s_waitcnt lgkmcnt(13)
	v_pk_add_f32 v[70:71], v[18:19], v[34:35]
	v_mov_b32_e32 v17, v164
	v_pk_add_f32 v[18:19], v[18:19], v[34:35] neg_lo:[0,1] neg_hi:[0,1]
	v_mov_b32_e32 v17, v166
	s_waitcnt lgkmcnt(12)
	v_pk_add_f32 v[34:35], v[20:21], v[36:37]
	v_pk_add_f32 v[20:21], v[20:21], v[36:37] neg_lo:[0,1] neg_hi:[0,1]
	v_mov_b32_e32 v17, v168
	s_nop 0
	v_pk_mul_f32 v[36:37], v[20:21], v[68:69] op_sel:[1,0] op_sel_hi:[0,0] neg_lo:[1,1] neg_hi:[0,1]
	v_mov_b32_e32 v17, v170
	v_pk_fma_f32 v[20:21], v[20:21], v[64:65], v[36:37] op_sel_hi:[1,0,1]
	s_waitcnt lgkmcnt(5)
	v_pk_add_f32 v[36:37], v[22:23], v[38:39]
	v_pk_add_f32 v[22:23], v[22:23], v[38:39] neg_lo:[0,1] neg_hi:[0,1]
	v_pk_mul_f32 v[38:39], v[22:23], v[66:67] op_sel:[1,0] op_sel_hi:[0,0] neg_lo:[1,1] neg_hi:[0,1]
	v_mov_b32_e32 v17, v171
	v_pk_fma_f32 v[22:23], v[22:23], v[66:67], v[38:39] op_sel_hi:[1,0,1]
	s_waitcnt lgkmcnt(4)
	v_pk_add_f32 v[38:39], v[24:25], v[40:41]
	v_pk_add_f32 v[24:25], v[24:25], v[40:41] neg_lo:[0,1] neg_hi:[0,1]
	v_pk_mul_f32 v[40:41], v[24:25], v[68:69] op_sel_hi:[1,0]
	v_pk_fma_f32 v[24:25], v[24:25], v[64:65], v[40:41] op_sel:[1,0,0] op_sel_hi:[0,0,1] neg_lo:[1,1,0] neg_hi:[0,1,0]
	s_waitcnt lgkmcnt(3)
	v_pk_add_f32 v[40:41], v[26:27], v[42:43]
	v_pk_add_f32 v[26:27], v[26:27], v[42:43] neg_lo:[0,1] neg_hi:[0,1]
	v_xor_b32_e32 v73, 0x80000000, v26
	v_mov_b32_e32 v72, v27
	s_waitcnt lgkmcnt(2)
	v_pk_add_f32 v[26:27], v[28:29], v[44:45]
	v_pk_add_f32 v[28:29], v[28:29], v[44:45] neg_lo:[0,1] neg_hi:[0,1]
	v_pk_mul_f32 v[42:43], v[28:29], v[68:69] op_sel_hi:[1,0] neg_lo:[0,1] neg_hi:[0,1]
	v_pk_fma_f32 v[28:29], v[28:29], v[64:65], v[42:43] op_sel:[1,0,0] op_sel_hi:[0,0,1] neg_lo:[1,1,0] neg_hi:[0,1,0]
	s_waitcnt lgkmcnt(1)
	v_pk_add_f32 v[42:43], v[30:31], v[46:47]
	v_pk_add_f32 v[30:31], v[30:31], v[46:47] neg_lo:[0,1] neg_hi:[0,1]
	v_pk_mul_f32 v[44:45], v[30:31], v[66:67] op_sel:[1,0] op_sel_hi:[0,0] neg_lo:[1,1] neg_hi:[0,1]
	v_pk_fma_f32 v[30:31], v[30:31], v[66:67], v[44:45] op_sel_hi:[1,0,1] neg_lo:[0,1,0] neg_hi:[0,1,0]
	s_waitcnt lgkmcnt(0)
	v_pk_add_f32 v[44:45], v[32:33], v[48:49]
	v_pk_add_f32 v[32:33], v[32:33], v[48:49] neg_lo:[0,1] neg_hi:[0,1]
	v_pk_add_f32 v[48:49], v[34:35], v[26:27]
	v_pk_add_f32 v[26:27], v[34:35], v[26:27] neg_lo:[0,1] neg_hi:[0,1]
	v_pk_mul_f32 v[34:35], v[26:27], v[66:67] op_sel:[1,0] op_sel_hi:[0,0] neg_lo:[1,1] neg_hi:[0,1]
	v_pk_fma_f32 v[26:27], v[26:27], v[66:67], v[34:35] op_sel_hi:[1,0,1]
	v_pk_add_f32 v[34:35], v[36:37], v[42:43]
	v_pk_add_f32 v[36:37], v[36:37], v[42:43] neg_lo:[0,1] neg_hi:[0,1]
	v_pk_mul_f32 v[46:47], v[32:33], v[68:69] op_sel:[1,0] op_sel_hi:[0,0] neg_lo:[1,1] neg_hi:[0,1]
	v_xor_b32_e32 v43, 0x80000000, v36
	v_mov_b32_e32 v42, v37
	v_pk_add_f32 v[36:37], v[38:39], v[44:45]
	v_pk_add_f32 v[38:39], v[38:39], v[44:45] neg_lo:[0,1] neg_hi:[0,1]
	v_pk_fma_f32 v[46:47], v[32:33], v[64:65], v[46:47] op_sel_hi:[1,0,1] neg_lo:[0,1,0] neg_hi:[0,1,0]
	v_pk_add_f32 v[32:33], v[70:71], v[40:41]
	v_pk_mul_f32 v[44:45], v[38:39], v[66:67] op_sel:[1,0] op_sel_hi:[0,0] neg_lo:[1,1] neg_hi:[0,1]
	v_pk_add_f32 v[40:41], v[70:71], v[40:41] neg_lo:[0,1] neg_hi:[0,1]
	v_pk_fma_f32 v[38:39], v[38:39], v[66:67], v[44:45] op_sel_hi:[1,0,1] neg_lo:[0,1,0] neg_hi:[0,1,0]
	v_pk_add_f32 v[44:45], v[32:33], v[34:35]
	v_pk_add_f32 v[32:33], v[32:33], v[34:35] neg_lo:[0,1] neg_hi:[0,1]
	v_pk_add_f32 v[34:35], v[48:49], v[36:37]
	v_pk_add_f32 v[36:37], v[48:49], v[36:37] neg_lo:[0,1] neg_hi:[0,1]
	v_pk_add_f32 v[64:65], v[44:45], v[34:35]
	v_xor_b32_e32 v49, 0x80000000, v36
	v_mov_b32_e32 v48, v37
	v_pk_add_f32 v[36:37], v[44:45], v[34:35] neg_lo:[0,1] neg_hi:[0,1]
	v_pk_add_f32 v[68:69], v[32:33], v[48:49]
	v_pk_add_f32 v[44:45], v[32:33], v[48:49] neg_lo:[0,1] neg_hi:[0,1]
	v_pk_add_f32 v[32:33], v[40:41], v[42:43]
	v_pk_add_f32 v[34:35], v[40:41], v[42:43] neg_lo:[0,1] neg_hi:[0,1]
	v_pk_add_f32 v[40:41], v[26:27], v[38:39]
	v_pk_add_f32 v[26:27], v[26:27], v[38:39] neg_lo:[0,1] neg_hi:[0,1]
	v_pk_add_f32 v[42:43], v[32:33], v[40:41] neg_lo:[0,1] neg_hi:[0,1]
	v_xor_b32_e32 v39, 0x80000000, v26
	v_mov_b32_e32 v38, v27
	v_pk_add_f32 v[26:27], v[32:33], v[40:41]
	v_pk_add_f32 v[40:41], v[20:21], v[28:29]
	v_pk_add_f32 v[20:21], v[20:21], v[28:29] neg_lo:[0,1] neg_hi:[0,1]
	v_pk_add_f32 v[32:33], v[34:35], v[38:39]
	v_pk_mul_f32 v[28:29], v[66:67], v[20:21] op_sel:[0,1] op_sel_hi:[0,0] neg_lo:[1,1] neg_hi:[1,0]
	v_pk_fma_f32 v[20:21], v[66:67], v[20:21], v[28:29] op_sel_hi:[0,1,1]
	v_pk_add_f32 v[28:29], v[22:23], v[30:31]
	v_pk_add_f32 v[22:23], v[22:23], v[30:31] neg_lo:[0,1] neg_hi:[0,1]
	v_pk_add_f32 v[38:39], v[34:35], v[38:39] neg_lo:[0,1] neg_hi:[0,1]
	v_xor_b32_e32 v31, 0x80000000, v22
	v_mov_b32_e32 v30, v23
	v_pk_add_f32 v[22:23], v[24:25], v[46:47]
	v_pk_add_f32 v[24:25], v[24:25], v[46:47] neg_lo:[0,1] neg_hi:[0,1]
	v_pk_add_f32 v[34:35], v[18:19], v[72:73]
	v_pk_mul_f32 v[46:47], v[66:67], v[24:25] op_sel:[0,1] op_sel_hi:[0,0] neg_lo:[1,1] neg_hi:[1,0]
	v_pk_fma_f32 v[24:25], v[66:67], v[24:25], v[46:47] op_sel_hi:[0,1,1] neg_lo:[1,0,0] neg_hi:[1,0,0]
	v_pk_add_f32 v[46:47], v[34:35], v[28:29]
	v_pk_add_f32 v[28:29], v[34:35], v[28:29] neg_lo:[0,1] neg_hi:[0,1]
	v_pk_add_f32 v[34:35], v[40:41], v[22:23]
	v_pk_add_f32 v[22:23], v[40:41], v[22:23] neg_lo:[0,1] neg_hi:[0,1]
	v_pk_add_f32 v[18:19], v[18:19], v[72:73] neg_lo:[0,1] neg_hi:[0,1]
	v_pk_add_f32 v[66:67], v[28:29], v[22:23] op_sel:[0,1] op_sel_hi:[1,0] neg_hi:[0,1]
	v_pk_add_f32 v[48:49], v[28:29], v[22:23] op_sel:[0,1] op_sel_hi:[1,0] neg_lo:[0,1]
	v_pk_add_f32 v[28:29], v[18:19], v[30:31]
	v_pk_add_f32 v[18:19], v[18:19], v[30:31] neg_lo:[0,1] neg_hi:[0,1]
	v_pk_add_f32 v[30:31], v[20:21], v[24:25]
	v_pk_add_f32 v[20:21], v[20:21], v[24:25] neg_lo:[0,1] neg_hi:[0,1]
	v_pk_add_f32 v[22:23], v[46:47], v[34:35]
	v_xor_b32_e32 v25, 0x80000000, v20
	v_add_u32_e32 v20, 0x2000, v16
	v_mov_b32_e32 v24, v21
	v_ashrrev_i32_e32 v21, 31, v20
	v_lshl_add_u64 v[20:21], v[20:21], 3, s[46:47]
	s_waitcnt vmcnt(0)
	v_pk_add_f32 v[40:41], v[46:47], v[34:35] neg_lo:[0,1] neg_hi:[0,1]
	v_pk_add_f32 v[34:35], v[18:19], v[24:25]
	v_pk_add_f32 v[18:19], v[18:19], v[24:25] neg_lo:[0,1] neg_hi:[0,1]
	v_pk_add_f32 v[70:71], v[28:29], v[30:31]
	v_pk_add_f32 v[46:47], v[28:29], v[30:31] neg_lo:[0,1] neg_hi:[0,1]
	s_nop 0
	v_pk_mul_f32 v[24:25], v[64:65], v[202:203] op_sel:[1,1] op_sel_hi:[1,0] neg_lo:[1,0]
	v_pk_fma_f32 v[20:21], v[64:65], v[202:203], v[24:25] op_sel_hi:[0,1,1]
	v_add_u32_e32 v24, 0x2200, v16
	v_ashrrev_i32_e32 v25, 31, v24
	v_lshl_add_u64 v[24:25], v[24:25], 3, s[46:47]
	s_nop 0
	v_pk_mul_f32 v[28:29], v[204:205], v[22:23] op_sel:[1,1] op_sel_hi:[0,1] neg_lo:[0,1]
	v_pk_fma_f32 v[22:23], v[204:205], v[22:23], v[28:29] op_sel_hi:[1,0,1]
	v_add_u32_e32 v24, 0x2400, v16
	v_ashrrev_i32_e32 v25, 31, v24
	v_lshl_add_u64 v[24:25], v[24:25], 3, s[46:47]
	s_nop 0
	v_pk_mul_f32 v[28:29], v[26:27], v[206:207] op_sel:[1,1] op_sel_hi:[1,0] neg_lo:[1,0]
	v_pk_fma_f32 v[24:25], v[26:27], v[206:207], v[28:29] op_sel_hi:[0,1,1]
	v_add_u32_e32 v26, 0x2600, v16
	v_ashrrev_i32_e32 v27, 31, v26
	v_lshl_add_u64 v[26:27], v[26:27], 3, s[46:47]
	s_nop 0
	v_pk_mul_f32 v[28:29], v[208:209], v[70:71] op_sel:[1,1] op_sel_hi:[0,1] neg_lo:[0,1]
	v_pk_fma_f32 v[26:27], v[208:209], v[70:71], v[28:29] op_sel_hi:[1,0,1]
	v_add_u32_e32 v28, 0x2800, v16
	v_ashrrev_i32_e32 v29, 31, v28
	v_lshl_add_u64 v[28:29], v[28:29], 3, s[46:47]
	s_nop 0
	v_pk_mul_f32 v[30:31], v[68:69], v[210:211] op_sel:[1,1] op_sel_hi:[1,0] neg_lo:[1,0]
	v_pk_fma_f32 v[28:29], v[68:69], v[210:211], v[30:31] op_sel_hi:[0,1,1]
	v_add_u32_e32 v30, 0x2a00, v16
	v_ashrrev_i32_e32 v31, 31, v30
	v_lshl_add_u64 v[30:31], v[30:31], 3, s[46:47]
	s_nop 0
	v_pk_mul_f32 v[64:65], v[212:213], v[66:67] op_sel:[1,1] op_sel_hi:[0,1] neg_lo:[0,1]
	v_pk_fma_f32 v[30:31], v[212:213], v[66:67], v[64:65] op_sel_hi:[1,0,1]
	v_add_u32_e32 v64, 0x2c00, v16
	v_ashrrev_i32_e32 v65, 31, v64
	v_lshl_add_u64 v[64:65], v[64:65], 3, s[46:47]
	s_nop 0
	v_pk_mul_f32 v[66:67], v[32:33], v[214:215] op_sel:[1,1] op_sel_hi:[1,0] neg_lo:[1,0]
	v_pk_fma_f32 v[32:33], v[32:33], v[214:215], v[66:67] op_sel_hi:[0,1,1]
	v_add_u32_e32 v64, 0x2e00, v16
	v_ashrrev_i32_e32 v65, 31, v64
	v_lshl_add_u64 v[64:65], v[64:65], 3, s[46:47]
	s_nop 0
	v_pk_mul_f32 v[66:67], v[216:217], v[34:35] op_sel:[1,1] op_sel_hi:[0,1] neg_lo:[0,1]
	v_pk_fma_f32 v[34:35], v[216:217], v[34:35], v[66:67] op_sel_hi:[1,0,1]
	v_add_u32_e32 v64, 0x3000, v16
	v_ashrrev_i32_e32 v65, 31, v64
	v_lshl_add_u64 v[64:65], v[64:65], 3, s[46:47]
	s_nop 0
	v_pk_mul_f32 v[66:67], v[36:37], v[218:219] op_sel:[1,1] op_sel_hi:[1,0] neg_lo:[1,0]
	v_pk_fma_f32 v[36:37], v[36:37], v[218:219], v[66:67] op_sel_hi:[0,1,1]
	v_add_u32_e32 v64, 0x3200, v16
	v_ashrrev_i32_e32 v65, 31, v64
	v_lshl_add_u64 v[64:65], v[64:65], 3, s[46:47]
	v_pk_add_f32 v[68:69], v[20:21], v[36:37]
	v_pk_add_f32 v[20:21], v[20:21], v[36:37] neg_lo:[0,1] neg_hi:[0,1]
	s_nop 0
	v_pk_mul_f32 v[66:67], v[40:41], v[220:221] op_sel:[1,1] op_sel_hi:[1,0] neg_lo:[1,0]
	v_pk_fma_f32 v[40:41], v[40:41], v[220:221], v[66:67] op_sel_hi:[0,1,1]
	v_add_u32_e32 v64, 0x3400, v16
	v_ashrrev_i32_e32 v65, 31, v64
	v_lshl_add_u64 v[64:65], v[64:65], 3, s[46:47]
	v_pk_add_f32 v[36:37], v[22:23], v[40:41]
	v_pk_add_f32 v[22:23], v[22:23], v[40:41] neg_lo:[0,1] neg_hi:[0,1]
	s_nop 0
	v_pk_mul_f32 v[66:67], v[42:43], v[222:223] op_sel:[1,1] op_sel_hi:[1,0] neg_lo:[1,0]
	v_pk_fma_f32 v[42:43], v[42:43], v[222:223], v[66:67] op_sel_hi:[0,1,1]
	v_add_u32_e32 v64, 0x3600, v16
	v_ashrrev_i32_e32 v65, 31, v64
	v_lshl_add_u64 v[64:65], v[64:65], 3, s[46:47]
	s_nop 0
	v_pk_mul_f32 v[66:67], v[46:47], v[224:225] op_sel:[1,1] op_sel_hi:[1,0] neg_lo:[1,0]
	v_pk_fma_f32 v[46:47], v[46:47], v[224:225], v[66:67] op_sel_hi:[0,1,1]
	v_add_u32_e32 v64, 0x3800, v16
	v_ashrrev_i32_e32 v65, 31, v64
	v_lshl_add_u64 v[64:65], v[64:65], 3, s[46:47]
	s_nop 0
	v_pk_mul_f32 v[66:67], v[44:45], v[226:227] op_sel:[1,1] op_sel_hi:[1,0] neg_lo:[1,0]
	v_pk_fma_f32 v[44:45], v[44:45], v[226:227], v[66:67] op_sel_hi:[0,1,1]
	v_add_u32_e32 v64, 0x3a00, v16
	v_ashrrev_i32_e32 v65, 31, v64
	v_lshl_add_u64 v[64:65], v[64:65], 3, s[46:47]
	s_nop 0
	v_pk_mul_f32 v[66:67], v[48:49], v[228:229] op_sel:[1,1] op_sel_hi:[1,0] neg_lo:[1,0]
	v_pk_fma_f32 v[48:49], v[48:49], v[228:229], v[66:67] op_sel_hi:[0,1,1]
	v_add_u32_e32 v64, 0x3c00, v16
	v_ashrrev_i32_e32 v65, 31, v64
	v_lshl_add_u64 v[64:65], v[64:65], 3, s[46:47]
	v_add_u32_e32 v16, 0x3e00, v16
	v_ashrrev_i32_e32 v17, 31, v16
	v_lshl_add_u64 v[16:17], v[16:17], 3, s[46:47]
	s_nop 0
	v_pk_mul_f32 v[66:67], v[38:39], v[230:231] op_sel:[1,1] op_sel_hi:[1,0] neg_lo:[1,0]
	v_pk_fma_f32 v[38:39], v[38:39], v[230:231], v[66:67] op_sel_hi:[0,1,1]
	s_nop 0
	v_pk_mul_f32 v[64:65], v[18:19], v[232:233] op_sel:[1,1] op_sel_hi:[1,0] neg_lo:[1,0]
	v_mov_b32_e32 v66, v169
	v_pk_fma_f32 v[16:17], v[18:19], v[232:233], v[64:65] op_sel_hi:[0,1,1]
	v_mov_b32_e32 v18, v1
	v_mov_b32_e32 v19, v166
	v_mov_b32_e32 v18, v164
	v_mov_b32_e32 v64, v167
	v_mov_b32_e32 v18, v165
	s_nop 0
	v_mov_b32_e32 v19, v168
	s_nop 0
	v_mov_b32_e32 v19, v170
	v_pk_mul_f32 v[40:41], v[22:23], v[66:67] op_sel:[1,0] op_sel_hi:[0,0] neg_lo:[1,0]
	v_mov_b32_e32 v19, v171
	s_nop 0
	v_pk_fma_f32 v[22:23], v[22:23], v[18:19], v[40:41] op_sel_hi:[1,0,1]
	v_pk_add_f32 v[40:41], v[24:25], v[42:43]
	v_pk_add_f32 v[24:25], v[24:25], v[42:43] neg_lo:[0,1] neg_hi:[0,1]
	v_pk_mul_f32 v[42:43], v[24:25], v[64:65] op_sel:[1,0] op_sel_hi:[0,0] neg_lo:[1,0]
	v_pk_fma_f32 v[24:25], v[24:25], v[64:65], v[42:43] op_sel_hi:[1,0,1]
	v_pk_add_f32 v[42:43], v[26:27], v[46:47]
	v_pk_add_f32 v[26:27], v[26:27], v[46:47] neg_lo:[0,1] neg_hi:[0,1]
	v_pk_mul_f32 v[46:47], v[26:27], v[66:67] op_sel_hi:[1,0]
	v_pk_fma_f32 v[26:27], v[26:27], v[18:19], v[46:47] op_sel:[1,0,0] op_sel_hi:[0,0,1] neg_lo:[1,0,0]
	v_pk_add_f32 v[46:47], v[28:29], v[44:45]
	v_pk_add_f32 v[28:29], v[28:29], v[44:45] neg_lo:[0,1] neg_hi:[0,1]
	v_xor_b32_e32 v44, 0x80000000, v29
	v_mov_b32_e32 v45, v28
	v_pk_add_f32 v[28:29], v[30:31], v[48:49]
	v_pk_add_f32 v[30:31], v[30:31], v[48:49] neg_lo:[0,1] neg_hi:[0,1]
	v_pk_mul_f32 v[48:49], v[30:31], v[66:67] op_sel_hi:[1,0] neg_lo:[0,1] neg_hi:[0,1]
	v_pk_fma_f32 v[30:31], v[30:31], v[18:19], v[48:49] op_sel:[1,0,0] op_sel_hi:[0,0,1] neg_lo:[1,0,0]
	v_pk_add_f32 v[48:49], v[32:33], v[38:39]
	v_pk_add_f32 v[32:33], v[32:33], v[38:39] neg_lo:[0,1] neg_hi:[0,1]
	v_pk_mul_f32 v[38:39], v[32:33], v[64:65] op_sel:[1,0] op_sel_hi:[0,0] neg_lo:[1,0]
	v_pk_fma_f32 v[32:33], v[32:33], v[64:65], v[38:39] op_sel_hi:[1,0,1] neg_lo:[0,1,0] neg_hi:[0,1,0]
	v_pk_add_f32 v[38:39], v[34:35], v[16:17]
	v_pk_add_f32 v[16:17], v[34:35], v[16:17] neg_lo:[0,1] neg_hi:[0,1]
	v_pk_mul_f32 v[34:35], v[16:17], v[66:67] op_sel:[1,0] op_sel_hi:[0,0] neg_lo:[1,0]
	v_pk_fma_f32 v[16:17], v[16:17], v[18:19], v[34:35] op_sel_hi:[1,0,1] neg_lo:[0,1,0] neg_hi:[0,1,0]
	v_pk_add_f32 v[18:19], v[68:69], v[46:47]
	v_pk_add_f32 v[34:35], v[68:69], v[46:47] neg_lo:[0,1] neg_hi:[0,1]
	v_pk_add_f32 v[46:47], v[36:37], v[28:29]
	v_pk_add_f32 v[28:29], v[36:37], v[28:29] neg_lo:[0,1] neg_hi:[0,1]
	v_pk_mul_f32 v[36:37], v[28:29], v[64:65] op_sel:[1,0] op_sel_hi:[0,0] neg_lo:[1,0]
	v_pk_fma_f32 v[28:29], v[28:29], v[64:65], v[36:37] op_sel_hi:[1,0,1]
	v_pk_add_f32 v[36:37], v[40:41], v[48:49]
	v_pk_add_f32 v[40:41], v[40:41], v[48:49] neg_lo:[0,1] neg_hi:[0,1]
	v_xor_b32_e32 v48, 0x80000000, v41
	v_mov_b32_e32 v49, v40
	v_pk_add_f32 v[40:41], v[42:43], v[38:39]
	v_pk_add_f32 v[38:39], v[42:43], v[38:39] neg_lo:[0,1] neg_hi:[0,1]
	v_pk_mul_f32 v[42:43], v[64:65], v[38:39] op_sel:[0,1] op_sel_hi:[0,0] neg_lo:[0,1]
	v_pk_fma_f32 v[38:39], v[38:39], v[64:65], v[42:43] op_sel_hi:[1,0,1] neg_lo:[0,1,0] neg_hi:[0,1,0]
	v_pk_add_f32 v[42:43], v[18:19], v[36:37]
	v_pk_add_f32 v[18:19], v[18:19], v[36:37] neg_lo:[0,1] neg_hi:[0,1]
	v_pk_add_f32 v[36:37], v[46:47], v[40:41]
	v_pk_add_f32 v[40:41], v[46:47], v[40:41] neg_lo:[0,1] neg_hi:[0,1]
	v_xor_b32_e32 v46, 0x80000000, v41
	v_mov_b32_e32 v47, v40
	v_pk_add_f32 v[40:41], v[42:43], v[36:37]
	v_pk_add_f32 v[36:37], v[42:43], v[36:37] neg_lo:[0,1] neg_hi:[0,1]
	v_pk_add_f32 v[42:43], v[18:19], v[46:47]
	v_pk_add_f32 v[18:19], v[18:19], v[46:47] neg_lo:[0,1] neg_hi:[0,1]
	v_pk_add_f32 v[46:47], v[34:35], v[48:49]
	v_pk_add_f32 v[34:35], v[34:35], v[48:49] neg_lo:[0,1] neg_hi:[0,1]
	v_pk_add_f32 v[48:49], v[28:29], v[38:39]
	v_pk_add_f32 v[28:29], v[28:29], v[38:39] neg_lo:[0,1] neg_hi:[0,1]
	v_xor_b32_e32 v38, 0x80000000, v29
	v_mov_b32_e32 v39, v28
	v_pk_add_f32 v[28:29], v[46:47], v[48:49]
	v_pk_add_f32 v[46:47], v[46:47], v[48:49] neg_lo:[0,1] neg_hi:[0,1]
	v_pk_add_f32 v[48:49], v[34:35], v[38:39]
	v_pk_add_f32 v[34:35], v[34:35], v[38:39] neg_lo:[0,1] neg_hi:[0,1]
	v_pk_add_f32 v[38:39], v[20:21], v[44:45]
	v_pk_add_f32 v[20:21], v[20:21], v[44:45] neg_lo:[0,1] neg_hi:[0,1]
	v_pk_add_f32 v[44:45], v[22:23], v[30:31]
	v_pk_add_f32 v[22:23], v[22:23], v[30:31] neg_lo:[0,1] neg_hi:[0,1]
	v_pk_mul_f32 v[30:31], v[64:65], v[22:23] op_sel:[0,1] op_sel_hi:[0,0] neg_lo:[0,1]
	v_pk_fma_f32 v[22:23], v[64:65], v[22:23], v[30:31] op_sel_hi:[0,1,1]
	v_pk_add_f32 v[30:31], v[24:25], v[32:33]
	v_pk_add_f32 v[24:25], v[24:25], v[32:33] neg_lo:[0,1] neg_hi:[0,1]
	v_xor_b32_e32 v32, 0x80000000, v25
	v_mov_b32_e32 v33, v24
	v_pk_add_f32 v[24:25], v[26:27], v[16:17]
	v_pk_add_f32 v[16:17], v[26:27], v[16:17] neg_lo:[0,1] neg_hi:[0,1]
	v_pk_mul_f32 v[26:27], v[64:65], v[16:17] op_sel:[0,1] op_sel_hi:[0,0] neg_lo:[0,1]
	v_pk_fma_f32 v[16:17], v[64:65], v[16:17], v[26:27] op_sel_hi:[0,1,1] neg_lo:[1,0,0] neg_hi:[1,0,0]
	v_pk_add_f32 v[26:27], v[38:39], v[30:31]
	v_pk_add_f32 v[30:31], v[38:39], v[30:31] neg_lo:[0,1] neg_hi:[0,1]
	v_pk_add_f32 v[38:39], v[44:45], v[24:25]
	v_pk_add_f32 v[24:25], v[44:45], v[24:25] neg_lo:[0,1] neg_hi:[0,1]
	v_xor_b32_e32 v44, 0x80000000, v25
	v_mov_b32_e32 v45, v24
	v_pk_add_f32 v[24:25], v[26:27], v[38:39]
	v_pk_add_f32 v[26:27], v[26:27], v[38:39] neg_lo:[0,1] neg_hi:[0,1]
	v_pk_add_f32 v[38:39], v[30:31], v[44:45]
	v_pk_add_f32 v[30:31], v[30:31], v[44:45] neg_lo:[0,1] neg_hi:[0,1]
	v_pk_add_f32 v[44:45], v[20:21], v[32:33]
	v_pk_add_f32 v[20:21], v[20:21], v[32:33] neg_lo:[0,1] neg_hi:[0,1]
	v_pk_add_f32 v[32:33], v[22:23], v[16:17]
	v_pk_add_f32 v[16:17], v[22:23], v[16:17] neg_lo:[0,1] neg_hi:[0,1]
	v_xor_b32_e32 v22, 0x80000000, v17
	v_mov_b32_e32 v23, v16
	v_pk_add_f32 v[16:17], v[44:45], v[32:33]
	v_pk_add_f32 v[32:33], v[44:45], v[32:33] neg_lo:[0,1] neg_hi:[0,1]
	v_pk_add_f32 v[44:45], v[20:21], v[22:23]
	v_pk_add_f32 v[20:21], v[20:21], v[22:23] neg_lo:[0,1] neg_hi:[0,1]
	ds_write_b64 v10, v[40:41]
	ds_write_b64 v13, v[24:25]
	ds_write_b64 v15, v[28:29]
	ds_write_b64 v50, v[16:17]
	ds_write_b64 v51, v[42:43]
	ds_write_b64 v52, v[38:39]
	ds_write_b64 v53, v[48:49]
	ds_write_b64 v54, v[44:45]
	ds_write_b64 v55, v[36:37]
	ds_write_b64 v56, v[26:27]
	ds_write_b64 v57, v[46:47]
	ds_write_b64 v58, v[32:33]
	ds_write_b64 v59, v[18:19]
	ds_write_b64 v60, v[30:31]
	ds_write_b64 v61, v[34:35]
	ds_write_b64 v62, v[20:21]
	v_mov_b32_e32 v10, v174
	v_mov_b32_e32 v50, v172
	s_waitcnt lgkmcnt(0)
	s_barrier
	v_add_u32_e32 v13, v50, v10
	v_lshl_add_u32 v13, v13, 3, 0
	ds_read2_b64 v[16:19], v13 offset1:16
	v_xad_u32 v15, v50, 1, v10
	v_lshl_add_u32 v15, v15, 3, 0
	s_waitcnt lgkmcnt(0)
	v_pk_fma_f32 v[16:17], v[16:17], 0, v[16:17] op_sel:[1,0,0] op_sel_hi:[0,0,1] neg_hi:[1,0,0]
	v_pk_fma_f32 v[22:23], v[180:181], s[90:91], v[180:181] op_sel:[1,0,0] op_sel_hi:[0,1,1]
	v_pk_mul_f32 v[24:25], v[22:23], v[18:19] op_sel:[1,1] op_sel_hi:[1,0] neg_hi:[0,1]
	v_pk_fma_f32 v[18:19], v[18:19], v[22:23], v[24:25] op_sel_hi:[1,0,1]
	v_pk_mul_f32 v[24:25], v[180:181], v[22:23] op_sel:[1,1] op_sel_hi:[0,1] neg_lo:[0,1]
	v_pk_fma_f32 v[26:27], v[180:181], v[22:23], v[24:25] op_sel_hi:[1,0,1]
	ds_read2_b64 v[22:25], v15 offset0:32 offset1:48
	s_waitcnt lgkmcnt(0)
	v_pk_mul_f32 v[28:29], v[22:23], v[26:27] op_sel:[1,1] op_sel_hi:[0,1] neg_hi:[1,0]
	v_pk_fma_f32 v[22:23], v[22:23], v[26:27], v[28:29] op_sel_hi:[1,0,1]
	v_pk_mul_f32 v[28:29], v[180:181], v[26:27] op_sel:[1,1] op_sel_hi:[0,1] neg_lo:[0,1]
	v_pk_fma_f32 v[26:27], v[180:181], v[26:27], v[28:29] op_sel_hi:[1,0,1]
	v_pk_mul_f32 v[28:29], v[24:25], v[26:27] op_sel:[1,1] op_sel_hi:[0,1] neg_hi:[1,0]
	v_pk_fma_f32 v[24:25], v[24:25], v[26:27], v[28:29] op_sel_hi:[1,0,1]
	v_pk_mul_f32 v[28:29], v[180:181], v[26:27] op_sel:[1,1] op_sel_hi:[0,1] neg_lo:[0,1]
	v_pk_fma_f32 v[26:27], v[180:181], v[26:27], v[28:29] op_sel_hi:[1,0,1]
	v_xad_u32 v28, v50, 2, v10
	v_lshl_add_u32 v51, v28, 3, 0
	ds_read2_b64 v[28:31], v51 offset0:64 offset1:80
	v_pk_mul_f32 v[32:33], v[180:181], v[26:27] op_sel:[1,1] op_sel_hi:[0,1] neg_lo:[0,1]
	s_waitcnt lgkmcnt(0)
	v_pk_mul_f32 v[34:35], v[28:29], v[26:27] op_sel:[1,1] op_sel_hi:[0,1] neg_hi:[1,0]
	v_pk_fma_f32 v[28:29], v[28:29], v[26:27], v[34:35] op_sel_hi:[1,0,1]
	v_pk_fma_f32 v[34:35], v[180:181], v[26:27], v[32:33] op_sel_hi:[1,0,1]
	v_pk_mul_f32 v[26:27], v[30:31], v[34:35] op_sel:[1,1] op_sel_hi:[0,1] neg_hi:[1,0]
	v_pk_fma_f32 v[26:27], v[30:31], v[34:35], v[26:27] op_sel_hi:[1,0,1]
	v_xad_u32 v30, v50, 3, v10
	v_lshl_add_u32 v54, v30, 3, 0
	ds_read2_b64 v[30:33], v54 offset0:96 offset1:112
	v_pk_mul_f32 v[36:37], v[180:181], v[34:35] op_sel:[1,1] op_sel_hi:[0,1] neg_lo:[0,1]
	v_pk_fma_f32 v[34:35], v[180:181], v[34:35], v[36:37] op_sel_hi:[1,0,1]
	s_waitcnt lgkmcnt(0)
	v_pk_mul_f32 v[36:37], v[30:31], v[34:35] op_sel:[1,1] op_sel_hi:[0,1] neg_hi:[1,0]
	v_pk_fma_f32 v[30:31], v[30:31], v[34:35], v[36:37] op_sel_hi:[1,0,1]
	v_pk_mul_f32 v[36:37], v[180:181], v[34:35] op_sel:[1,1] op_sel_hi:[0,1] neg_lo:[0,1]
	v_pk_fma_f32 v[34:35], v[180:181], v[34:35], v[36:37] op_sel_hi:[1,0,1]
	v_pk_mul_f32 v[36:37], v[32:33], v[34:35] op_sel:[1,1] op_sel_hi:[0,1] neg_hi:[1,0]
	v_pk_fma_f32 v[32:33], v[32:33], v[34:35], v[36:37] op_sel_hi:[1,0,1]
	v_pk_mul_f32 v[36:37], v[180:181], v[34:35] op_sel:[1,1] op_sel_hi:[0,1] neg_lo:[0,1]
	v_pk_fma_f32 v[38:39], v[180:181], v[34:35], v[36:37] op_sel_hi:[1,0,1]
	v_xad_u32 v34, v50, 4, v10
	v_lshl_add_u32 v55, v34, 3, 0
	ds_read2_b64 v[34:37], v55 offset0:128 offset1:144
	v_pk_mul_f32 v[40:41], v[180:181], v[38:39] op_sel:[1,1] op_sel_hi:[0,1] neg_lo:[0,1]
	s_waitcnt lgkmcnt(0)
	v_pk_mul_f32 v[42:43], v[34:35], v[38:39] op_sel:[1,1] op_sel_hi:[0,1] neg_hi:[1,0]
	v_pk_fma_f32 v[34:35], v[34:35], v[38:39], v[42:43] op_sel_hi:[1,0,1]
	v_pk_fma_f32 v[42:43], v[180:181], v[38:39], v[40:41] op_sel_hi:[1,0,1]
	v_pk_mul_f32 v[38:39], v[36:37], v[42:43] op_sel:[1,1] op_sel_hi:[0,1] neg_hi:[1,0]
	v_pk_fma_f32 v[36:37], v[36:37], v[42:43], v[38:39] op_sel_hi:[1,0,1]
	v_xad_u32 v38, v50, 5, v10
	v_lshl_add_u32 v56, v38, 3, 0
	ds_read2_b64 v[38:41], v56 offset0:160 offset1:176
	v_pk_mul_f32 v[44:45], v[180:181], v[42:43] op_sel:[1,1] op_sel_hi:[0,1] neg_lo:[0,1]
	v_pk_fma_f32 v[42:43], v[180:181], v[42:43], v[44:45] op_sel_hi:[1,0,1]
	s_waitcnt lgkmcnt(0)
	v_pk_mul_f32 v[44:45], v[38:39], v[42:43] op_sel:[1,1] op_sel_hi:[0,1] neg_hi:[1,0]
	v_pk_fma_f32 v[38:39], v[38:39], v[42:43], v[44:45] op_sel_hi:[1,0,1]
	v_pk_mul_f32 v[44:45], v[180:181], v[42:43] op_sel:[1,1] op_sel_hi:[0,1] neg_lo:[0,1]
	v_pk_fma_f32 v[42:43], v[180:181], v[42:43], v[44:45] op_sel_hi:[1,0,1]
	v_pk_mul_f32 v[44:45], v[40:41], v[42:43] op_sel:[1,1] op_sel_hi:[0,1] neg_hi:[1,0]
	v_pk_fma_f32 v[40:41], v[40:41], v[42:43], v[44:45] op_sel_hi:[1,0,1]
	v_pk_mul_f32 v[44:45], v[180:181], v[42:43] op_sel:[1,1] op_sel_hi:[0,1] neg_lo:[0,1]
	v_pk_fma_f32 v[42:43], v[180:181], v[42:43], v[44:45] op_sel_hi:[1,0,1]
	v_xad_u32 v44, v50, 6, v10
	v_lshl_add_u32 v57, v44, 3, 0
	ds_read2_b64 v[44:47], v57 offset0:192 offset1:208
	v_pk_mul_f32 v[48:49], v[180:181], v[42:43] op_sel:[1,1] op_sel_hi:[0,1] neg_lo:[0,1]
	s_waitcnt lgkmcnt(0)
	v_pk_mul_f32 v[52:53], v[44:45], v[42:43] op_sel:[1,1] op_sel_hi:[0,1] neg_hi:[1,0]
	v_pk_fma_f32 v[44:45], v[44:45], v[42:43], v[52:53] op_sel_hi:[1,0,1]
	v_pk_fma_f32 v[52:53], v[180:181], v[42:43], v[48:49] op_sel_hi:[1,0,1]
	v_pk_mul_f32 v[42:43], v[46:47], v[52:53] op_sel:[1,1] op_sel_hi:[0,1] neg_hi:[1,0]
	v_pk_fma_f32 v[42:43], v[46:47], v[52:53], v[42:43] op_sel_hi:[1,0,1]
	v_xad_u32 v46, v50, 7, v10
	v_lshl_add_u32 v58, v46, 3, 0
	ds_read2_b64 v[46:49], v58 offset0:224 offset1:240
	v_pk_mul_f32 v[60:61], v[180:181], v[52:53] op_sel:[1,1] op_sel_hi:[0,1] neg_lo:[0,1]
	v_pk_fma_f32 v[52:53], v[180:181], v[52:53], v[60:61] op_sel_hi:[1,0,1]
	s_waitcnt lgkmcnt(0)
	v_pk_mul_f32 v[60:61], v[46:47], v[52:53] op_sel:[1,1] op_sel_hi:[0,1] neg_hi:[1,0]
	v_pk_fma_f32 v[46:47], v[46:47], v[52:53], v[60:61] op_sel_hi:[1,0,1]
	v_pk_mul_f32 v[60:61], v[180:181], v[52:53] op_sel:[1,1] op_sel_hi:[0,1] neg_lo:[0,1]
	v_pk_fma_f32 v[52:53], v[180:181], v[52:53], v[60:61] op_sel_hi:[1,0,1]
	v_pk_mul_f32 v[60:61], v[48:49], v[52:53] op_sel:[1,1] op_sel_hi:[0,1] neg_hi:[1,0]
	v_pk_fma_f32 v[48:49], v[48:49], v[52:53], v[60:61] op_sel_hi:[1,0,1]
	v_pk_mul_f32 v[60:61], v[180:181], v[52:53] op_sel:[1,1] op_sel_hi:[0,1] neg_lo:[0,1]
	v_pk_fma_f32 v[64:65], v[180:181], v[52:53], v[60:61] op_sel_hi:[1,0,1]
	v_xad_u32 v52, v50, 8, v10
	v_lshl_add_u32 v52, v52, 3, 0
	v_add_u32_e32 v59, 0x800, v52
	ds_read2_b64 v[60:63], v59 offset1:16
	v_pk_mul_f32 v[66:67], v[180:181], v[64:65] op_sel:[1,1] op_sel_hi:[0,1] neg_lo:[0,1]
	v_pk_fma_f32 v[66:67], v[180:181], v[64:65], v[66:67] op_sel_hi:[1,0,1]
	s_waitcnt lgkmcnt(0)
	v_pk_mul_f32 v[52:53], v[60:61], v[64:65] op_sel:[1,1] op_sel_hi:[0,1] neg_hi:[1,0]
	v_pk_fma_f32 v[52:53], v[60:61], v[64:65], v[52:53] op_sel_hi:[1,0,1]
	v_pk_mul_f32 v[60:61], v[62:63], v[66:67] op_sel:[1,1] op_sel_hi:[0,1] neg_hi:[1,0]
	v_pk_fma_f32 v[70:71], v[62:63], v[66:67], v[60:61] op_sel_hi:[1,0,1]
	v_xad_u32 v60, v50, 9, v10
	v_lshl_add_u32 v60, v60, 3, 0
	v_add_u32_e32 v60, 0x800, v60
	ds_read2_b64 v[62:65], v60 offset0:32 offset1:48
	v_pk_mul_f32 v[68:69], v[180:181], v[66:67] op_sel:[1,1] op_sel_hi:[0,1] neg_lo:[0,1]
	v_pk_fma_f32 v[66:67], v[180:181], v[66:67], v[68:69] op_sel_hi:[1,0,1]
	s_waitcnt lgkmcnt(0)
	v_pk_mul_f32 v[68:69], v[62:63], v[66:67] op_sel:[1,1] op_sel_hi:[0,1] neg_hi:[1,0]
	v_pk_fma_f32 v[72:73], v[62:63], v[66:67], v[68:69] op_sel_hi:[1,0,1]
	v_pk_mul_f32 v[62:63], v[180:181], v[66:67] op_sel:[1,1] op_sel_hi:[0,1] neg_lo:[0,1]
	v_pk_fma_f32 v[62:63], v[180:181], v[66:67], v[62:63] op_sel_hi:[1,0,1]
	v_pk_mul_f32 v[66:67], v[64:65], v[62:63] op_sel:[1,1] op_sel_hi:[0,1] neg_hi:[1,0]
	v_pk_fma_f32 v[74:75], v[64:65], v[62:63], v[66:67] op_sel_hi:[1,0,1]
	v_pk_mul_f32 v[64:65], v[180:181], v[62:63] op_sel:[1,1] op_sel_hi:[0,1] neg_lo:[0,1]
	v_pk_fma_f32 v[66:67], v[180:181], v[62:63], v[64:65] op_sel_hi:[1,0,1]
	v_xad_u32 v61, v50, 10, v10
	v_lshl_add_u32 v61, v61, 3, 0
	v_add_u32_e32 v61, 0x800, v61
	ds_read2_b64 v[62:65], v61 offset0:64 offset1:80
	v_pk_mul_f32 v[68:69], v[180:181], v[66:67] op_sel:[1,1] op_sel_hi:[0,1] neg_lo:[0,1]
	v_pk_fma_f32 v[68:69], v[180:181], v[66:67], v[68:69] op_sel_hi:[1,0,1]
	s_waitcnt lgkmcnt(0)
	v_pk_mul_f32 v[76:77], v[62:63], v[66:67] op_sel:[1,1] op_sel_hi:[0,1] neg_hi:[1,0]
	v_pk_fma_f32 v[76:77], v[62:63], v[66:67], v[76:77] op_sel_hi:[1,0,1]
	v_pk_mul_f32 v[62:63], v[64:65], v[68:69] op_sel:[1,1] op_sel_hi:[0,1] neg_hi:[1,0]
	v_pk_fma_f32 v[78:79], v[64:65], v[68:69], v[62:63] op_sel_hi:[1,0,1]
	v_xad_u32 v62, v50, 11, v10
	v_lshl_add_u32 v62, v62, 3, 0
	v_add_u32_e32 v62, 0x800, v62
	ds_read2_b64 v[64:67], v62 offset0:96 offset1:112
	v_pk_mul_f32 v[80:81], v[180:181], v[68:69] op_sel:[1,1] op_sel_hi:[0,1] neg_lo:[0,1]
	v_pk_fma_f32 v[68:69], v[180:181], v[68:69], v[80:81] op_sel_hi:[1,0,1]
	s_waitcnt lgkmcnt(0)
	v_pk_mul_f32 v[80:81], v[64:65], v[68:69] op_sel:[1,1] op_sel_hi:[0,1] neg_hi:[1,0]
	v_pk_fma_f32 v[80:81], v[64:65], v[68:69], v[80:81] op_sel_hi:[1,0,1]
	v_pk_mul_f32 v[64:65], v[180:181], v[68:69] op_sel:[1,1] op_sel_hi:[0,1] neg_lo:[0,1]
	v_pk_fma_f32 v[64:65], v[180:181], v[68:69], v[64:65] op_sel_hi:[1,0,1]
	v_pk_mul_f32 v[68:69], v[66:67], v[64:65] op_sel:[1,1] op_sel_hi:[0,1] neg_hi:[1,0]
	v_pk_fma_f32 v[82:83], v[66:67], v[64:65], v[68:69] op_sel_hi:[1,0,1]
	v_pk_mul_f32 v[66:67], v[180:181], v[64:65] op_sel:[1,1] op_sel_hi:[0,1] neg_lo:[0,1]
	v_pk_fma_f32 v[68:69], v[180:181], v[64:65], v[66:67] op_sel_hi:[1,0,1]
	v_xad_u32 v63, v50, 12, v10
	v_lshl_add_u32 v63, v63, 3, 0
	v_add_u32_e32 v63, 0x800, v63
	ds_read2_b64 v[64:67], v63 offset0:128 offset1:144
	v_pk_mul_f32 v[84:85], v[180:181], v[68:69] op_sel:[1,1] op_sel_hi:[0,1] neg_lo:[0,1]
	v_pk_fma_f32 v[84:85], v[180:181], v[68:69], v[84:85] op_sel_hi:[1,0,1]
	s_waitcnt lgkmcnt(0)
	v_pk_mul_f32 v[86:87], v[64:65], v[68:69] op_sel:[1,1] op_sel_hi:[0,1] neg_hi:[1,0]
	v_pk_fma_f32 v[86:87], v[64:65], v[68:69], v[86:87] op_sel_hi:[1,0,1]
	v_pk_mul_f32 v[64:65], v[66:67], v[84:85] op_sel:[1,1] op_sel_hi:[0,1] neg_hi:[1,0]
	v_pk_fma_f32 v[88:89], v[66:67], v[84:85], v[64:65] op_sel_hi:[1,0,1]
	v_xad_u32 v64, v50, 13, v10
	v_lshl_add_u32 v64, v64, 3, 0
	v_add_u32_e32 v64, 0x800, v64
	ds_read2_b64 v[66:69], v64 offset0:160 offset1:176
	v_pk_mul_f32 v[90:91], v[180:181], v[84:85] op_sel:[1,1] op_sel_hi:[0,1] neg_lo:[0,1]
	v_pk_fma_f32 v[84:85], v[180:181], v[84:85], v[90:91] op_sel_hi:[1,0,1]
	s_waitcnt lgkmcnt(0)
	v_pk_mul_f32 v[90:91], v[66:67], v[84:85] op_sel:[1,1] op_sel_hi:[0,1] neg_hi:[1,0]
	v_pk_fma_f32 v[90:91], v[66:67], v[84:85], v[90:91] op_sel_hi:[1,0,1]
	v_pk_mul_f32 v[66:67], v[180:181], v[84:85] op_sel:[1,1] op_sel_hi:[0,1] neg_lo:[0,1]
	v_pk_fma_f32 v[66:67], v[180:181], v[84:85], v[66:67] op_sel_hi:[1,0,1]
	v_pk_mul_f32 v[84:85], v[68:69], v[66:67] op_sel:[1,1] op_sel_hi:[0,1] neg_hi:[1,0]
	v_pk_fma_f32 v[84:85], v[68:69], v[66:67], v[84:85] op_sel_hi:[1,0,1]
	v_pk_mul_f32 v[68:69], v[180:181], v[66:67] op_sel:[1,1] op_sel_hi:[0,1] neg_lo:[0,1]
	v_pk_fma_f32 v[92:93], v[180:181], v[66:67], v[68:69] op_sel_hi:[1,0,1]
	v_xad_u32 v65, v50, 14, v10
	v_lshl_add_u32 v65, v65, 3, 0
	v_add_u32_e32 v65, 0x800, v65
	ds_read2_b64 v[66:69], v65 offset0:192 offset1:208
	v_pk_mul_f32 v[94:95], v[180:181], v[92:93] op_sel:[1,1] op_sel_hi:[0,1] neg_lo:[0,1]
	v_xad_u32 v10, v50, 15, v10
	s_waitcnt lgkmcnt(0)
	v_pk_mul_f32 v[96:97], v[66:67], v[92:93] op_sel:[1,1] op_sel_hi:[0,1] neg_hi:[1,0]
	v_lshl_add_u32 v10, v10, 3, 0
	v_pk_fma_f32 v[96:97], v[66:67], v[92:93], v[96:97] op_sel_hi:[1,0,1]
	v_pk_fma_f32 v[92:93], v[180:181], v[92:93], v[94:95] op_sel_hi:[1,0,1]
	v_pk_mul_f32 v[66:67], v[68:69], v[92:93] op_sel:[1,1] op_sel_hi:[0,1] neg_hi:[1,0]
	v_add_u32_e32 v101, 0x800, v10
	v_pk_fma_f32 v[94:95], v[68:69], v[92:93], v[66:67] op_sel_hi:[1,0,1]
	ds_read2_b64 v[66:69], v101 offset0:224 offset1:240
	v_pk_mul_f32 v[98:99], v[180:181], v[92:93] op_sel:[1,1] op_sel_hi:[0,1] neg_lo:[0,1]
	v_pk_fma_f32 v[92:93], v[180:181], v[92:93], v[98:99] op_sel_hi:[1,0,1]
	s_waitcnt lgkmcnt(0)
	v_pk_mul_f32 v[98:99], v[66:67], v[92:93] op_sel:[1,1] op_sel_hi:[0,1] neg_hi:[1,0]
	v_pk_fma_f32 v[66:67], v[66:67], v[92:93], v[98:99] op_sel_hi:[1,0,1]
	v_pk_mul_f32 v[98:99], v[180:181], v[92:93] op_sel:[1,1] op_sel_hi:[0,1] neg_lo:[0,1]
	v_pk_fma_f32 v[20:21], v[180:181], v[92:93], v[98:99] op_sel_hi:[1,0,1]
	v_pk_mul_f32 v[92:93], v[68:69], v[20:21] op_sel:[1,1] op_sel_hi:[0,1] neg_hi:[1,0]
	v_pk_fma_f32 v[68:69], v[68:69], v[20:21], v[92:93] op_sel_hi:[1,0,1]
	v_mov_b32_e32 v10, v1
	v_pk_add_f32 v[104:105], v[16:17], v[52:53]
	v_pk_add_f32 v[16:17], v[16:17], v[52:53] neg_lo:[0,1] neg_hi:[0,1]
	v_pk_add_f32 v[52:53], v[18:19], v[70:71]
	v_pk_add_f32 v[18:19], v[18:19], v[70:71] neg_lo:[0,1] neg_hi:[0,1]
	v_mov_b32_e32 v92, v164
	v_mov_b32_e32 v20, v165
	v_mov_b32_e32 v98, v166
	v_mov_b32_e32 v10, v167
	v_mov_b32_e32 v100, v168
	v_mov_b32_e32 v50, v169
	v_mov_b32_e32 v102, v170
	v_mov_b32_e32 v21, v171
	v_pk_mul_f32 v[70:71], v[102:103], v[18:19] op_sel:[0,1] op_sel_hi:[0,0] neg_lo:[0,1]
	v_pk_fma_f32 v[18:19], v[92:93], v[18:19], v[70:71] op_sel_hi:[0,1,1]
	v_pk_add_f32 v[70:71], v[22:23], v[72:73]
	v_pk_add_f32 v[22:23], v[22:23], v[72:73] neg_lo:[0,1] neg_hi:[0,1]
	v_pk_mul_f32 v[72:73], v[50:51], v[22:23] op_sel:[0,1] op_sel_hi:[0,0] neg_lo:[0,1]
	v_pk_fma_f32 v[22:23], v[20:21], v[22:23], v[72:73] op_sel_hi:[0,1,1]
	v_pk_add_f32 v[72:73], v[24:25], v[74:75]
	v_pk_add_f32 v[24:25], v[24:25], v[74:75] neg_lo:[0,1] neg_hi:[0,1]
	v_pk_mul_f32 v[74:75], v[100:101], v[24:25] op_sel:[0,1] op_sel_hi:[0,0] neg_lo:[0,1]
	v_pk_fma_f32 v[24:25], v[98:99], v[24:25], v[74:75] op_sel_hi:[0,1,1]
	v_pk_add_f32 v[74:75], v[28:29], v[76:77]
	v_pk_add_f32 v[28:29], v[28:29], v[76:77] neg_lo:[0,1] neg_hi:[0,1]
	v_pk_mul_f32 v[76:77], v[10:11], v[28:29] op_sel:[0,1] op_sel_hi:[0,0] neg_lo:[0,1]
	v_pk_fma_f32 v[28:29], v[10:11], v[28:29], v[76:77] op_sel_hi:[0,1,1]
	v_pk_add_f32 v[76:77], v[26:27], v[78:79]
	v_pk_add_f32 v[26:27], v[26:27], v[78:79] neg_lo:[0,1] neg_hi:[0,1]
	v_pk_mul_f32 v[78:79], v[98:99], v[26:27] op_sel:[0,1] op_sel_hi:[0,0] neg_lo:[0,1]
	v_pk_fma_f32 v[26:27], v[100:101], v[26:27], v[78:79] op_sel_hi:[0,1,1]
	v_pk_add_f32 v[78:79], v[30:31], v[80:81]
	v_pk_add_f32 v[30:31], v[30:31], v[80:81] neg_lo:[0,1] neg_hi:[0,1]
	v_pk_mul_f32 v[80:81], v[20:21], v[30:31] op_sel:[0,1] op_sel_hi:[0,0] neg_lo:[0,1]
	v_pk_fma_f32 v[30:31], v[50:51], v[30:31], v[80:81] op_sel_hi:[0,1,1]
	v_pk_add_f32 v[80:81], v[32:33], v[82:83]
	v_pk_add_f32 v[32:33], v[32:33], v[82:83] neg_lo:[0,1] neg_hi:[0,1]
	v_pk_mul_f32 v[82:83], v[92:93], v[32:33] op_sel:[0,1] op_sel_hi:[0,0] neg_lo:[0,1]
	v_pk_fma_f32 v[32:33], v[102:103], v[32:33], v[82:83] op_sel_hi:[0,1,1]
	v_pk_add_f32 v[82:83], v[34:35], v[86:87]
	v_pk_add_f32 v[34:35], v[34:35], v[86:87] neg_lo:[0,1] neg_hi:[0,1]
	v_xor_b32_e32 v86, 0x80000000, v35
	v_mov_b32_e32 v87, v34
	v_pk_add_f32 v[34:35], v[36:37], v[88:89]
	v_pk_add_f32 v[36:37], v[36:37], v[88:89] neg_lo:[0,1] neg_hi:[0,1]
	v_pk_mul_f32 v[88:89], v[92:93], v[36:37] op_sel:[0,1] op_sel_hi:[0,0] neg_lo:[0,1]
	v_pk_fma_f32 v[36:37], v[102:103], v[36:37], v[88:89] op_sel_hi:[0,1,1] neg_lo:[1,0,0] neg_hi:[1,0,0]
	v_pk_add_f32 v[88:89], v[38:39], v[90:91]
	v_pk_add_f32 v[38:39], v[38:39], v[90:91] neg_lo:[0,1] neg_hi:[0,1]
	v_pk_mul_f32 v[90:91], v[20:21], v[38:39] op_sel:[0,1] op_sel_hi:[0,0] neg_lo:[0,1]
	v_pk_fma_f32 v[38:39], v[50:51], v[38:39], v[90:91] op_sel_hi:[0,1,1] neg_lo:[1,0,0] neg_hi:[1,0,0]
	v_pk_add_f32 v[90:91], v[40:41], v[84:85]
	v_pk_add_f32 v[40:41], v[40:41], v[84:85] neg_lo:[0,1] neg_hi:[0,1]
	v_pk_mul_f32 v[84:85], v[98:99], v[40:41] op_sel:[0,1] op_sel_hi:[0,0] neg_lo:[0,1]
	v_pk_fma_f32 v[40:41], v[100:101], v[40:41], v[84:85] op_sel_hi:[0,1,1] neg_lo:[1,0,0] neg_hi:[1,0,0]
	v_pk_add_f32 v[84:85], v[44:45], v[96:97]
	v_pk_add_f32 v[44:45], v[44:45], v[96:97] neg_lo:[0,1] neg_hi:[0,1]
	v_pk_mul_f32 v[96:97], v[10:11], v[44:45] op_sel:[0,1] op_sel_hi:[0,0] neg_lo:[0,1]
	v_pk_fma_f32 v[44:45], v[10:11], v[44:45], v[96:97] op_sel_hi:[0,1,1] neg_lo:[1,0,0] neg_hi:[1,0,0]
	v_pk_add_f32 v[96:97], v[42:43], v[94:95]
	v_pk_add_f32 v[42:43], v[42:43], v[94:95] neg_lo:[0,1] neg_hi:[0,1]
	v_pk_mul_f32 v[94:95], v[100:101], v[42:43] op_sel:[0,1] op_sel_hi:[0,0] neg_lo:[0,1]
	v_pk_fma_f32 v[42:43], v[98:99], v[42:43], v[94:95] op_sel_hi:[0,1,1] neg_lo:[1,0,0] neg_hi:[1,0,0]
	v_pk_add_f32 v[94:95], v[46:47], v[66:67]
	v_pk_add_f32 v[46:47], v[46:47], v[66:67] neg_lo:[0,1] neg_hi:[0,1]
	v_pk_mul_f32 v[66:67], v[50:51], v[46:47] op_sel:[0,1] op_sel_hi:[0,0] neg_lo:[0,1]
	v_pk_fma_f32 v[46:47], v[20:21], v[46:47], v[66:67] op_sel_hi:[0,1,1] neg_lo:[1,0,0] neg_hi:[1,0,0]
	v_pk_add_f32 v[66:67], v[48:49], v[68:69]
	v_pk_add_f32 v[48:49], v[48:49], v[68:69] neg_lo:[0,1] neg_hi:[0,1]
	v_pk_mul_f32 v[68:69], v[102:103], v[48:49] op_sel:[0,1] op_sel_hi:[0,0] neg_lo:[0,1]
	v_pk_fma_f32 v[48:49], v[92:93], v[48:49], v[68:69] op_sel_hi:[0,1,1] neg_lo:[1,0,0] neg_hi:[1,0,0]
	v_pk_add_f32 v[92:93], v[52:53], v[34:35]
	v_pk_add_f32 v[34:35], v[52:53], v[34:35] neg_lo:[0,1] neg_hi:[0,1]
	v_pk_add_f32 v[68:69], v[104:105], v[82:83]
	v_pk_mul_f32 v[52:53], v[50:51], v[34:35] op_sel:[0,1] op_sel_hi:[0,0] neg_lo:[0,1]
	v_pk_fma_f32 v[34:35], v[20:21], v[34:35], v[52:53] op_sel_hi:[0,1,1]
	v_pk_add_f32 v[52:53], v[70:71], v[88:89]
	v_pk_add_f32 v[70:71], v[70:71], v[88:89] neg_lo:[0,1] neg_hi:[0,1]
	v_pk_add_f32 v[82:83], v[104:105], v[82:83] neg_lo:[0,1] neg_hi:[0,1]
	v_pk_mul_f32 v[88:89], v[10:11], v[70:71] op_sel:[0,1] op_sel_hi:[0,0] neg_lo:[0,1]
	v_pk_fma_f32 v[70:71], v[10:11], v[70:71], v[88:89] op_sel_hi:[0,1,1]
	v_pk_add_f32 v[88:89], v[72:73], v[90:91]
	v_pk_add_f32 v[72:73], v[72:73], v[90:91] neg_lo:[0,1] neg_hi:[0,1]
	v_pk_mul_f32 v[90:91], v[20:21], v[72:73] op_sel:[0,1] op_sel_hi:[0,0] neg_lo:[0,1]
	v_pk_fma_f32 v[72:73], v[50:51], v[72:73], v[90:91] op_sel_hi:[0,1,1]
	v_pk_add_f32 v[90:91], v[74:75], v[84:85]
	v_pk_add_f32 v[74:75], v[74:75], v[84:85] neg_lo:[0,1] neg_hi:[0,1]
	v_xor_b32_e32 v84, 0x80000000, v75
	v_mov_b32_e32 v85, v74
	v_pk_add_f32 v[74:75], v[76:77], v[96:97]
	v_pk_add_f32 v[76:77], v[76:77], v[96:97] neg_lo:[0,1] neg_hi:[0,1]
	v_pk_mul_f32 v[96:97], v[20:21], v[76:77] op_sel:[0,1] op_sel_hi:[0,0] neg_lo:[0,1]
	v_pk_fma_f32 v[76:77], v[50:51], v[76:77], v[96:97] op_sel_hi:[0,1,1] neg_lo:[1,0,0] neg_hi:[1,0,0]
	v_pk_add_f32 v[96:97], v[78:79], v[94:95]
	v_pk_add_f32 v[78:79], v[78:79], v[94:95] neg_lo:[0,1] neg_hi:[0,1]
	v_pk_mul_f32 v[94:95], v[10:11], v[78:79] op_sel:[0,1] op_sel_hi:[0,0] neg_lo:[0,1]
	v_pk_fma_f32 v[78:79], v[10:11], v[78:79], v[94:95] op_sel_hi:[0,1,1] neg_lo:[1,0,0] neg_hi:[1,0,0]
	v_pk_add_f32 v[94:95], v[80:81], v[66:67]
	v_pk_add_f32 v[66:67], v[80:81], v[66:67] neg_lo:[0,1] neg_hi:[0,1]
	v_pk_mul_f32 v[80:81], v[50:51], v[66:67] op_sel:[0,1] op_sel_hi:[0,0] neg_lo:[0,1]
	v_pk_fma_f32 v[66:67], v[20:21], v[66:67], v[80:81] op_sel_hi:[0,1,1] neg_lo:[1,0,0] neg_hi:[1,0,0]
	v_pk_add_f32 v[80:81], v[68:69], v[90:91]
	v_pk_add_f32 v[68:69], v[68:69], v[90:91] neg_lo:[0,1] neg_hi:[0,1]
	v_pk_add_f32 v[90:91], v[92:93], v[74:75]
	v_pk_add_f32 v[74:75], v[92:93], v[74:75] neg_lo:[0,1] neg_hi:[0,1]
	v_pk_mul_f32 v[92:93], v[10:11], v[74:75] op_sel:[0,1] op_sel_hi:[0,0] neg_lo:[0,1]
	v_pk_fma_f32 v[74:75], v[10:11], v[74:75], v[92:93] op_sel_hi:[0,1,1]
	v_pk_add_f32 v[92:93], v[52:53], v[96:97]
	v_pk_add_f32 v[52:53], v[52:53], v[96:97] neg_lo:[0,1] neg_hi:[0,1]
	v_xor_b32_e32 v96, 0x80000000, v53
	v_mov_b32_e32 v97, v52
	v_pk_add_f32 v[52:53], v[88:89], v[94:95]
	v_pk_add_f32 v[88:89], v[88:89], v[94:95] neg_lo:[0,1] neg_hi:[0,1]
	v_pk_mul_f32 v[94:95], v[10:11], v[88:89] op_sel:[0,1] op_sel_hi:[0,0] neg_lo:[0,1]
	v_pk_fma_f32 v[88:89], v[10:11], v[88:89], v[94:95] op_sel_hi:[0,1,1] neg_lo:[1,0,0] neg_hi:[1,0,0]
	v_pk_add_f32 v[94:95], v[80:81], v[92:93]
	v_pk_add_f32 v[80:81], v[80:81], v[92:93] neg_lo:[0,1] neg_hi:[0,1]
	v_pk_add_f32 v[92:93], v[90:91], v[52:53]
	v_pk_add_f32 v[52:53], v[90:91], v[52:53] neg_lo:[0,1] neg_hi:[0,1]
	v_xor_b32_e32 v90, 0x80000000, v53
	v_mov_b32_e32 v91, v52
	v_pk_add_f32 v[52:53], v[94:95], v[92:93]
	v_pk_add_f32 v[92:93], v[94:95], v[92:93] neg_lo:[0,1] neg_hi:[0,1]
	v_pk_add_f32 v[94:95], v[80:81], v[90:91]
	v_pk_add_f32 v[80:81], v[80:81], v[90:91] neg_lo:[0,1] neg_hi:[0,1]
	v_pk_add_f32 v[90:91], v[68:69], v[96:97]
	v_pk_add_f32 v[68:69], v[68:69], v[96:97] neg_lo:[0,1] neg_hi:[0,1]
	v_pk_add_f32 v[96:97], v[74:75], v[88:89]
	v_pk_add_f32 v[74:75], v[74:75], v[88:89] neg_lo:[0,1] neg_hi:[0,1]
	v_xor_b32_e32 v88, 0x80000000, v75
	v_mov_b32_e32 v89, v74
	v_pk_add_f32 v[74:75], v[90:91], v[96:97]
	v_pk_add_f32 v[90:91], v[90:91], v[96:97] neg_lo:[0,1] neg_hi:[0,1]
	v_pk_add_f32 v[96:97], v[68:69], v[88:89]
	v_pk_add_f32 v[68:69], v[68:69], v[88:89] neg_lo:[0,1] neg_hi:[0,1]
	v_pk_add_f32 v[88:89], v[82:83], v[84:85]
	v_pk_add_f32 v[82:83], v[82:83], v[84:85] neg_lo:[0,1] neg_hi:[0,1]
	v_pk_add_f32 v[84:85], v[34:35], v[76:77]
	v_pk_add_f32 v[34:35], v[34:35], v[76:77] neg_lo:[0,1] neg_hi:[0,1]
	v_pk_mul_f32 v[76:77], v[10:11], v[34:35] op_sel:[0,1] op_sel_hi:[0,0] neg_lo:[0,1]
	v_pk_fma_f32 v[34:35], v[10:11], v[34:35], v[76:77] op_sel_hi:[0,1,1]
	v_pk_add_f32 v[76:77], v[70:71], v[78:79]
	v_pk_add_f32 v[70:71], v[70:71], v[78:79] neg_lo:[0,1] neg_hi:[0,1]
	v_xor_b32_e32 v78, 0x80000000, v71
	v_mov_b32_e32 v79, v70
	v_pk_add_f32 v[70:71], v[72:73], v[66:67]
	v_pk_add_f32 v[66:67], v[72:73], v[66:67] neg_lo:[0,1] neg_hi:[0,1]
	v_pk_mul_f32 v[72:73], v[10:11], v[66:67] op_sel:[0,1] op_sel_hi:[0,0] neg_lo:[0,1]
	v_pk_fma_f32 v[66:67], v[10:11], v[66:67], v[72:73] op_sel_hi:[0,1,1] neg_lo:[1,0,0] neg_hi:[1,0,0]
	v_pk_add_f32 v[72:73], v[88:89], v[76:77]
	v_pk_add_f32 v[76:77], v[88:89], v[76:77] neg_lo:[0,1] neg_hi:[0,1]
	v_pk_add_f32 v[88:89], v[84:85], v[70:71]
	v_pk_add_f32 v[70:71], v[84:85], v[70:71] neg_lo:[0,1] neg_hi:[0,1]
	v_xor_b32_e32 v84, 0x80000000, v71
	v_mov_b32_e32 v85, v70
	v_pk_add_f32 v[70:71], v[72:73], v[88:89]
	v_pk_add_f32 v[72:73], v[72:73], v[88:89] neg_lo:[0,1] neg_hi:[0,1]
	v_pk_add_f32 v[88:89], v[76:77], v[84:85]
	v_pk_add_f32 v[76:77], v[76:77], v[84:85] neg_lo:[0,1] neg_hi:[0,1]
	v_pk_add_f32 v[84:85], v[82:83], v[78:79]
	v_pk_add_f32 v[78:79], v[82:83], v[78:79] neg_lo:[0,1] neg_hi:[0,1]
	v_pk_add_f32 v[82:83], v[34:35], v[66:67]
	v_pk_add_f32 v[34:35], v[34:35], v[66:67] neg_lo:[0,1] neg_hi:[0,1]
	v_xor_b32_e32 v66, 0x80000000, v35
	v_mov_b32_e32 v67, v34
	v_pk_add_f32 v[34:35], v[84:85], v[82:83]
	v_pk_add_f32 v[82:83], v[84:85], v[82:83] neg_lo:[0,1] neg_hi:[0,1]
	v_pk_add_f32 v[84:85], v[78:79], v[66:67]
	v_pk_add_f32 v[66:67], v[78:79], v[66:67] neg_lo:[0,1] neg_hi:[0,1]
	v_pk_add_f32 v[78:79], v[16:17], v[86:87]
	v_pk_add_f32 v[16:17], v[16:17], v[86:87] neg_lo:[0,1] neg_hi:[0,1]
	v_pk_add_f32 v[86:87], v[18:19], v[36:37]
	v_pk_add_f32 v[18:19], v[18:19], v[36:37] neg_lo:[0,1] neg_hi:[0,1]
	v_pk_mul_f32 v[36:37], v[50:51], v[18:19] op_sel:[0,1] op_sel_hi:[0,0] neg_lo:[0,1]
	v_pk_fma_f32 v[18:19], v[20:21], v[18:19], v[36:37] op_sel_hi:[0,1,1]
	v_pk_add_f32 v[36:37], v[22:23], v[38:39]
	v_pk_add_f32 v[22:23], v[22:23], v[38:39] neg_lo:[0,1] neg_hi:[0,1]
	v_pk_mul_f32 v[38:39], v[10:11], v[22:23] op_sel:[0,1] op_sel_hi:[0,0] neg_lo:[0,1]
	v_pk_fma_f32 v[22:23], v[10:11], v[22:23], v[38:39] op_sel_hi:[0,1,1]
	v_pk_add_f32 v[38:39], v[24:25], v[40:41]
	v_pk_add_f32 v[24:25], v[24:25], v[40:41] neg_lo:[0,1] neg_hi:[0,1]
	v_pk_mul_f32 v[40:41], v[20:21], v[24:25] op_sel:[0,1] op_sel_hi:[0,0] neg_lo:[0,1]
	v_pk_fma_f32 v[24:25], v[50:51], v[24:25], v[40:41] op_sel_hi:[0,1,1]
	v_pk_add_f32 v[40:41], v[28:29], v[44:45]
	v_pk_add_f32 v[28:29], v[28:29], v[44:45] neg_lo:[0,1] neg_hi:[0,1]
	v_xor_b32_e32 v44, 0x80000000, v29
	v_mov_b32_e32 v45, v28
	v_pk_add_f32 v[28:29], v[26:27], v[42:43]
	v_pk_add_f32 v[26:27], v[26:27], v[42:43] neg_lo:[0,1] neg_hi:[0,1]
	v_pk_mul_f32 v[42:43], v[20:21], v[26:27] op_sel:[0,1] op_sel_hi:[0,0] neg_lo:[0,1]
	v_pk_fma_f32 v[26:27], v[50:51], v[26:27], v[42:43] op_sel_hi:[0,1,1] neg_lo:[1,0,0] neg_hi:[1,0,0]
	v_pk_add_f32 v[42:43], v[30:31], v[46:47]
	v_pk_add_f32 v[30:31], v[30:31], v[46:47] neg_lo:[0,1] neg_hi:[0,1]
	v_pk_mul_f32 v[46:47], v[10:11], v[30:31] op_sel:[0,1] op_sel_hi:[0,0] neg_lo:[0,1]
	v_pk_fma_f32 v[30:31], v[10:11], v[30:31], v[46:47] op_sel_hi:[0,1,1] neg_lo:[1,0,0] neg_hi:[1,0,0]
	v_pk_add_f32 v[46:47], v[32:33], v[48:49]
	v_pk_add_f32 v[32:33], v[32:33], v[48:49] neg_lo:[0,1] neg_hi:[0,1]
	v_pk_mul_f32 v[48:49], v[50:51], v[32:33] op_sel:[0,1] op_sel_hi:[0,0] neg_lo:[0,1]
	v_pk_fma_f32 v[20:21], v[20:21], v[32:33], v[48:49] op_sel_hi:[0,1,1] neg_lo:[1,0,0] neg_hi:[1,0,0]
	v_pk_add_f32 v[48:49], v[86:87], v[28:29]
	v_pk_add_f32 v[28:29], v[86:87], v[28:29] neg_lo:[0,1] neg_hi:[0,1]
	v_pk_add_f32 v[32:33], v[78:79], v[40:41]
	v_pk_add_f32 v[40:41], v[78:79], v[40:41] neg_lo:[0,1] neg_hi:[0,1]
	v_pk_mul_f32 v[78:79], v[10:11], v[28:29] op_sel:[0,1] op_sel_hi:[0,0] neg_lo:[0,1]
	v_pk_fma_f32 v[28:29], v[10:11], v[28:29], v[78:79] op_sel_hi:[0,1,1]
	v_pk_add_f32 v[78:79], v[36:37], v[42:43]
	v_pk_add_f32 v[36:37], v[36:37], v[42:43] neg_lo:[0,1] neg_hi:[0,1]
	v_xor_b32_e32 v42, 0x80000000, v37
	v_mov_b32_e32 v43, v36
	v_pk_add_f32 v[36:37], v[38:39], v[46:47]
	v_pk_add_f32 v[38:39], v[38:39], v[46:47] neg_lo:[0,1] neg_hi:[0,1]
	v_pk_mul_f32 v[46:47], v[10:11], v[38:39] op_sel:[0,1] op_sel_hi:[0,0] neg_lo:[0,1]
	v_pk_fma_f32 v[38:39], v[10:11], v[38:39], v[46:47] op_sel_hi:[0,1,1] neg_lo:[1,0,0] neg_hi:[1,0,0]
	v_pk_add_f32 v[46:47], v[32:33], v[78:79]
	v_pk_add_f32 v[32:33], v[32:33], v[78:79] neg_lo:[0,1] neg_hi:[0,1]
	v_pk_add_f32 v[78:79], v[48:49], v[36:37]
	v_pk_add_f32 v[36:37], v[48:49], v[36:37] neg_lo:[0,1] neg_hi:[0,1]
	v_pk_add_f32 v[86:87], v[32:33], v[36:37] op_sel:[0,1] op_sel_hi:[1,0] neg_lo:[0,1]
	v_pk_add_f32 v[32:33], v[32:33], v[36:37] op_sel:[0,1] op_sel_hi:[1,0] neg_hi:[0,1]
	v_pk_add_f32 v[48:49], v[40:41], v[42:43]
	v_pk_add_f32 v[40:41], v[40:41], v[42:43] neg_lo:[0,1] neg_hi:[0,1]
	v_pk_add_f32 v[42:43], v[28:29], v[38:39]
	v_pk_add_f32 v[28:29], v[28:29], v[38:39] neg_lo:[0,1] neg_hi:[0,1]
	v_pk_add_f32 v[36:37], v[46:47], v[78:79] neg_lo:[0,1] neg_hi:[0,1]
	v_xor_b32_e32 v38, 0x80000000, v29
	v_mov_b32_e32 v39, v28
	v_pk_add_f32 v[28:29], v[48:49], v[42:43]
	v_pk_add_f32 v[42:43], v[48:49], v[42:43] neg_lo:[0,1] neg_hi:[0,1]
	v_pk_add_f32 v[48:49], v[40:41], v[38:39]
	v_pk_add_f32 v[38:39], v[40:41], v[38:39] neg_lo:[0,1] neg_hi:[0,1]
	v_pk_add_f32 v[40:41], v[16:17], v[44:45]
	v_pk_add_f32 v[16:17], v[16:17], v[44:45] neg_lo:[0,1] neg_hi:[0,1]
	v_pk_add_f32 v[44:45], v[18:19], v[26:27]
	v_pk_add_f32 v[18:19], v[18:19], v[26:27] neg_lo:[0,1] neg_hi:[0,1]
	v_pk_mul_f32 v[26:27], v[10:11], v[18:19] op_sel:[0,1] op_sel_hi:[0,0] neg_lo:[0,1]
	v_pk_fma_f32 v[18:19], v[10:11], v[18:19], v[26:27] op_sel_hi:[0,1,1]
	v_pk_add_f32 v[26:27], v[22:23], v[30:31]
	v_pk_add_f32 v[22:23], v[22:23], v[30:31] neg_lo:[0,1] neg_hi:[0,1]
	v_xor_b32_e32 v30, 0x80000000, v23
	v_mov_b32_e32 v31, v22
	v_pk_add_f32 v[22:23], v[24:25], v[20:21]
	v_pk_add_f32 v[20:21], v[24:25], v[20:21] neg_lo:[0,1] neg_hi:[0,1]
	v_pk_mul_f32 v[24:25], v[10:11], v[20:21] op_sel:[0,1] op_sel_hi:[0,0] neg_lo:[0,1]
	v_pk_fma_f32 v[20:21], v[10:11], v[20:21], v[24:25] op_sel_hi:[0,1,1] neg_lo:[1,0,0] neg_hi:[1,0,0]
	v_pk_add_f32 v[24:25], v[40:41], v[26:27]
	v_pk_add_f32 v[26:27], v[40:41], v[26:27] neg_lo:[0,1] neg_hi:[0,1]
	v_pk_add_f32 v[40:41], v[44:45], v[22:23]
	v_pk_add_f32 v[22:23], v[44:45], v[22:23] neg_lo:[0,1] neg_hi:[0,1]
	v_xor_b32_e32 v44, 0x80000000, v23
	v_mov_b32_e32 v45, v22
	v_pk_add_f32 v[22:23], v[24:25], v[40:41]
	v_pk_add_f32 v[24:25], v[24:25], v[40:41] neg_lo:[0,1] neg_hi:[0,1]
	v_pk_add_f32 v[40:41], v[26:27], v[44:45]
	v_pk_add_f32 v[26:27], v[26:27], v[44:45] neg_lo:[0,1] neg_hi:[0,1]
	v_pk_add_f32 v[44:45], v[16:17], v[30:31]
	v_pk_add_f32 v[16:17], v[16:17], v[30:31] neg_lo:[0,1] neg_hi:[0,1]
	v_pk_add_f32 v[30:31], v[18:19], v[20:21]
	v_pk_add_f32 v[18:19], v[18:19], v[20:21] neg_lo:[0,1] neg_hi:[0,1]
	v_xor_b32_e32 v20, 0x80000000, v19
	v_mov_b32_e32 v21, v18
	v_pk_add_f32 v[18:19], v[44:45], v[30:31]
	v_pk_add_f32 v[30:31], v[44:45], v[30:31] neg_lo:[0,1] neg_hi:[0,1]
	v_pk_add_f32 v[44:45], v[16:17], v[20:21]
	v_pk_add_f32 v[16:17], v[16:17], v[20:21] neg_lo:[0,1] neg_hi:[0,1]
	v_pk_add_f32 v[20:21], v[46:47], v[78:79]
	ds_write2_b64 v13, v[52:53], v[20:21] offset1:16
	ds_write2_b64 v15, v[70:71], v[22:23] offset0:32 offset1:48
	ds_write2_b64 v51, v[74:75], v[28:29] offset0:64 offset1:80
	ds_write2_b64 v54, v[34:35], v[18:19] offset0:96 offset1:112
	ds_write2_b64 v55, v[94:95], v[86:87] offset0:128 offset1:144
	ds_write2_b64 v56, v[88:89], v[40:41] offset0:160 offset1:176
	ds_write2_b64 v57, v[96:97], v[48:49] offset0:192 offset1:208
	ds_write2_b64 v58, v[84:85], v[44:45] offset0:224 offset1:240
	ds_write2_b64 v59, v[92:93], v[36:37] offset1:16
	ds_write2_b64 v60, v[72:73], v[24:25] offset0:32 offset1:48
	ds_write2_b64 v61, v[90:91], v[42:43] offset0:64 offset1:80
	ds_write2_b64 v62, v[82:83], v[30:31] offset0:96 offset1:112
	ds_write2_b64 v63, v[80:81], v[32:33] offset0:128 offset1:144
	ds_write2_b64 v64, v[76:77], v[26:27] offset0:160 offset1:176
	ds_write2_b64 v65, v[68:69], v[38:39] offset0:192 offset1:208
	ds_write2_b64 v101, v[66:67], v[16:17] offset0:224 offset1:240
	v_mov_b32_e32 v10, v173
	s_waitcnt lgkmcnt(0)
	s_barrier
	v_lshl_add_u32 v10, v10, 3, 0
	ds_read_b64 v[16:17], v10
	ds_read_b64 v[80:81], v10 offset:4224
	ds_read_b64 v[78:79], v10 offset:8448
	ds_read_b64 v[76:77], v10 offset:12672
	ds_read_b64 v[74:75], v10 offset:16896
	ds_read_b64 v[72:73], v10 offset:21120
	ds_read_b64 v[70:71], v10 offset:25344
	ds_read_b64 v[68:69], v10 offset:29568
	ds_read_b64 v[24:25], v10 offset:33792
	ds_read_b64 v[62:63], v10 offset:38016
	ds_read_b64 v[60:61], v10 offset:42240
	ds_read_b64 v[58:59], v10 offset:46464
	ds_read_b64 v[54:55], v10 offset:50688
	ds_read_b64 v[50:51], v10 offset:54912
	ds_read_b64 v[46:47], v10 offset:59136
	ds_read_b64 v[44:45], v10 offset:63360
	v_add_u32_e32 v13, 0x10800, v10
	v_add_u32_e32 v15, 0x11880, v10
	v_add_u32_e32 v20, 0x12900, v10
	v_add_u32_e32 v21, 0x13980, v10
	ds_read_b64 v[18:19], v13
	ds_read_b64 v[66:67], v15
	ds_read_b64 v[64:65], v20
	ds_read_b64 v[38:39], v21
	v_add_u32_e32 v13, 0x14a00, v10
	v_add_u32_e32 v15, 0x15a80, v10
	v_add_u32_e32 v20, 0x16b00, v10
	v_add_u32_e32 v21, 0x17b80, v10
	ds_read_b64 v[30:31], v13
	ds_read_b64 v[56:57], v15
	ds_read_b64 v[52:53], v20
	ds_read_b64 v[48:49], v21
	v_add_u32_e32 v13, 0x18c00, v10
	v_add_u32_e32 v15, 0x19c80, v10
	v_add_u32_e32 v20, 0x1ad00, v10
	v_add_u32_e32 v21, 0x1bd80, v10
	ds_read_b64 v[82:83], v13
	ds_read_b64 v[42:43], v15
	ds_read_b64 v[40:41], v20
	ds_read_b64 v[36:37], v21
	v_add_u32_e32 v13, 0x1ce00, v10
	v_add_u32_e32 v15, 0x1de80, v10
	v_add_u32_e32 v20, 0x1ef00, v10
	v_add_u32_e32 v10, 0x1ff80, v10
	ds_read_b64 v[34:35], v13
	ds_read_b64 v[32:33], v15
	ds_read_b64 v[28:29], v20
	ds_read_b64 v[26:27], v10
	v_pk_fma_f32 v[84:85], v[178:179], s[90:91], v[178:179] op_sel:[1,0,0] op_sel_hi:[0,1,1]
	v_pk_mul_f32 v[20:21], v[178:179], v[84:85] op_sel:[1,1] op_sel_hi:[0,1] neg_lo:[0,1]
	v_pk_fma_f32 v[86:87], v[178:179], v[84:85], v[20:21] op_sel_hi:[1,0,1]
	v_mov_b32_e32 v10, v1
	v_pk_mul_f32 v[20:21], v[178:179], v[86:87] op_sel:[1,1] op_sel_hi:[0,1] neg_lo:[0,1]
	v_pk_fma_f32 v[88:89], v[178:179], v[86:87], v[20:21] op_sel_hi:[1,0,1]
	v_mov_b32_e32 v13, v171
	v_pk_mul_f32 v[20:21], v[178:179], v[88:89] op_sel:[1,1] op_sel_hi:[0,1] neg_lo:[0,1]
	v_pk_fma_f32 v[90:91], v[178:179], v[88:89], v[20:21] op_sel_hi:[1,0,1]
	v_mov_b32_e32 v10, v164
	v_pk_mul_f32 v[20:21], v[178:179], v[90:91] op_sel:[1,1] op_sel_hi:[0,1] neg_lo:[0,1]
	v_pk_fma_f32 v[92:93], v[178:179], v[90:91], v[20:21] op_sel_hi:[1,0,1]
	s_waitcnt lgkmcnt(14)
	v_fmac_f32_e32 v16, 0, v17
	v_pk_mul_f32 v[20:21], v[178:179], v[92:93] op_sel:[1,1] op_sel_hi:[0,1] neg_lo:[0,1]
	v_pk_fma_f32 v[94:95], v[178:179], v[92:93], v[20:21] op_sel_hi:[1,0,1]
	v_readlane_b32 s70, v251, 22
	v_pk_mul_f32 v[20:21], v[178:179], v[94:95] op_sel:[1,1] op_sel_hi:[0,1] neg_lo:[0,1]
	v_pk_fma_f32 v[96:97], v[178:179], v[94:95], v[20:21] op_sel_hi:[1,0,1]
	v_readlane_b32 s71, v251, 23
	v_pk_mul_f32 v[20:21], v[178:179], v[96:97] op_sel:[1,1] op_sel_hi:[0,1] neg_lo:[0,1]
	v_pk_fma_f32 v[98:99], v[178:179], v[96:97], v[20:21] op_sel_hi:[1,0,1]
	s_movk_i32 s10, 0x1000
	v_pk_mul_f32 v[20:21], v[178:179], v[98:99] op_sel:[1,1] op_sel_hi:[0,1] neg_lo:[0,1]
	v_pk_fma_f32 v[100:101], v[178:179], v[98:99], v[20:21] op_sel_hi:[1,0,1]
	s_movk_i32 s11, 0x2000
	v_pk_mul_f32 v[20:21], v[178:179], v[100:101] op_sel:[1,1] op_sel_hi:[0,1] neg_lo:[0,1]
	v_pk_fma_f32 v[102:103], v[178:179], v[100:101], v[20:21] op_sel_hi:[1,0,1]
	s_movk_i32 s13, 0x5000
	v_pk_mul_f32 v[20:21], v[178:179], v[102:103] op_sel:[1,1] op_sel_hi:[0,1] neg_lo:[0,1]
	v_pk_fma_f32 v[104:105], v[178:179], v[102:103], v[20:21] op_sel_hi:[1,0,1]
	s_movk_i32 s12, 0x6000
	v_pk_mul_f32 v[20:21], v[178:179], v[104:105] op_sel:[1,1] op_sel_hi:[0,1] neg_lo:[0,1]
	v_pk_fma_f32 v[106:107], v[178:179], v[104:105], v[20:21] op_sel_hi:[1,0,1]
	s_movk_i32 s16, 0x7000
	v_pk_mul_f32 v[20:21], v[178:179], v[106:107] op_sel:[1,1] op_sel_hi:[0,1] neg_lo:[0,1]
	v_pk_fma_f32 v[108:109], v[178:179], v[106:107], v[20:21] op_sel_hi:[1,0,1]
	s_mov_b32 s80, 0x3f74fa0b
	v_pk_mul_f32 v[20:21], v[178:179], v[108:109] op_sel:[1,1] op_sel_hi:[0,1] neg_lo:[0,1]
	v_pk_fma_f32 v[110:111], v[178:179], v[108:109], v[20:21] op_sel_hi:[1,0,1]
	s_mov_b32 s81, 0xbe94a031
	v_pk_mul_f32 v[20:21], v[178:179], v[110:111] op_sel:[1,1] op_sel_hi:[0,1] neg_lo:[0,1]
	v_pk_fma_f32 v[112:113], v[178:179], v[110:111], v[20:21] op_sel_hi:[1,0,1]
	s_mov_b32 s20, 0x3f61c598
	v_pk_mul_f32 v[20:21], v[178:179], v[112:113] op_sel:[1,1] op_sel_hi:[0,1] neg_lo:[0,1]
	v_pk_fma_f32 v[20:21], v[178:179], v[112:113], v[20:21] op_sel_hi:[1,0,1]
	s_mov_b32 s21, 0xbef15aea
	v_pk_mul_f32 v[114:115], v[178:179], v[20:21] op_sel:[1,1] op_sel_hi:[0,1] neg_lo:[0,1]
	v_pk_fma_f32 v[114:115], v[178:179], v[20:21], v[114:115] op_sel_hi:[1,0,1]
	v_mul_f32_e32 v18, v18, v20
	v_pk_mul_f32 v[116:117], v[178:179], v[114:115] op_sel:[1,1] op_sel_hi:[0,1] neg_lo:[0,1]
	v_pk_fma_f32 v[116:117], v[178:179], v[114:115], v[116:117] op_sel_hi:[1,0,1]
	v_fmac_f32_e32 v18, v19, v21
	v_pk_mul_f32 v[118:119], v[178:179], v[116:117] op_sel:[1,1] op_sel_hi:[0,1] neg_lo:[0,1]
	v_pk_fma_f32 v[118:119], v[178:179], v[116:117], v[118:119] op_sel_hi:[1,0,1]
	v_add_f32_e32 v17, v16, v18
	v_pk_mul_f32 v[120:121], v[178:179], v[118:119] op_sel:[1,1] op_sel_hi:[0,1] neg_lo:[0,1]
	v_pk_fma_f32 v[120:121], v[178:179], v[118:119], v[120:121] op_sel_hi:[1,0,1]
	s_mov_b32 s40, s45
	v_pk_mul_f32 v[122:123], v[178:179], v[120:121] op_sel:[1,1] op_sel_hi:[0,1] neg_lo:[0,1]
	v_pk_fma_f32 v[122:123], v[178:179], v[120:121], v[122:123] op_sel_hi:[1,0,1]
	s_mov_b32 s41, s94
	v_pk_mul_f32 v[124:125], v[178:179], v[122:123] op_sel:[1,1] op_sel_hi:[0,1] neg_lo:[0,1]
	v_pk_fma_f32 v[124:125], v[178:179], v[122:123], v[124:125] op_sel_hi:[1,0,1]
	s_mov_b32 s86, 0x3f226799
	v_pk_mul_f32 v[126:127], v[178:179], v[124:125] op_sel:[1,1] op_sel_hi:[0,1] neg_lo:[0,1]
	v_pk_fma_f32 v[126:127], v[178:179], v[124:125], v[126:127] op_sel_hi:[1,0,1]
	s_mov_b32 s87, 0xbf45e403
	v_pk_mul_f32 v[128:129], v[178:179], v[126:127] op_sel:[1,1] op_sel_hi:[0,1] neg_lo:[0,1]
	v_pk_fma_f32 v[128:129], v[178:179], v[126:127], v[128:129] op_sel_hi:[1,0,1]
	s_mov_b32 s24, 0x3f0e39da
	v_pk_mul_f32 v[130:131], v[178:179], v[128:129] op_sel:[1,1] op_sel_hi:[0,1] neg_lo:[0,1]
	v_pk_fma_f32 v[130:131], v[178:179], v[128:129], v[130:131] op_sel_hi:[1,0,1]
	s_mov_b32 s25, 0xbf54db31
	v_pk_mul_f32 v[132:133], v[178:179], v[130:131] op_sel:[1,1] op_sel_hi:[0,1] neg_lo:[0,1]
	v_pk_fma_f32 v[132:133], v[178:179], v[130:131], v[132:133] op_sel_hi:[1,0,1]
	s_mov_b32 s88, 0x3ef15aea
	v_pk_mul_f32 v[134:135], v[178:179], v[132:133] op_sel:[1,1] op_sel_hi:[0,1] neg_lo:[0,1]
	v_pk_fma_f32 v[134:135], v[178:179], v[132:133], v[134:135] op_sel_hi:[1,0,1]
	s_mov_b32 s89, 0xbf61c598
	v_pk_mul_f32 v[136:137], v[178:179], v[134:135] op_sel:[1,1] op_sel_hi:[0,1] neg_lo:[0,1]
	v_pk_fma_f32 v[136:137], v[178:179], v[134:135], v[136:137] op_sel_hi:[1,0,1]
	s_mov_b32 s18, 0x3ec3ef15
	v_pk_mul_f32 v[138:139], v[178:179], v[136:137] op_sel:[1,1] op_sel_hi:[0,1] neg_lo:[0,1]
	v_pk_fma_f32 v[138:139], v[178:179], v[136:137], v[138:139] op_sel_hi:[1,0,1]
	s_mov_b32 s19, 0xbf6c835e
	v_pk_mul_f32 v[140:141], v[178:179], v[138:139] op_sel:[1,1] op_sel_hi:[0,1] neg_lo:[0,1]
	v_pk_fma_f32 v[140:141], v[178:179], v[138:139], v[140:141] op_sel_hi:[1,0,1]
	s_mov_b32 s92, 0x3e94a031
	v_pk_mul_f32 v[142:143], v[178:179], v[140:141] op_sel:[1,1] op_sel_hi:[0,1] neg_lo:[0,1]
	v_pk_fma_f32 v[22:23], v[178:179], v[140:141], v[142:143] op_sel_hi:[1,0,1]
	s_waitcnt lgkmcnt(0)
	v_pk_mul_f32 v[142:143], v[26:27], v[22:23] op_sel:[1,1] op_sel_hi:[0,1] neg_hi:[1,0]
	s_mov_b32 s93, 0xbf74fa0b
	v_pk_fma_f32 v[26:27], v[26:27], v[22:23], v[142:143] op_sel_hi:[1,0,1]
	v_pk_mul_f32 v[22:23], v[28:29], v[140:141] op_sel:[1,1] op_sel_hi:[0,1] neg_hi:[1,0]
	s_mov_b32 s82, 0x3f54db31
	v_pk_fma_f32 v[28:29], v[28:29], v[140:141], v[22:23] op_sel_hi:[1,0,1]
	v_pk_mul_f32 v[22:23], v[32:33], v[138:139] op_sel:[1,1] op_sel_hi:[0,1] neg_hi:[1,0]
	s_mov_b32 s83, 0xbf0e39da
	v_pk_fma_f32 v[32:33], v[32:33], v[138:139], v[22:23] op_sel_hi:[1,0,1]
	v_pk_mul_f32 v[22:23], v[34:35], v[136:137] op_sel:[1,1] op_sel_hi:[0,1] neg_hi:[1,0]
	s_mov_b32 s28, 0x3f45e403
	v_pk_fma_f32 v[34:35], v[34:35], v[136:137], v[22:23] op_sel_hi:[1,0,1]
	v_pk_mul_f32 v[22:23], v[36:37], v[134:135] op_sel:[1,1] op_sel_hi:[0,1] neg_hi:[1,0]
	s_mov_b32 s29, 0xbf226799
	v_pk_fma_f32 v[36:37], v[36:37], v[134:135], v[22:23] op_sel_hi:[1,0,1]
	v_pk_mul_f32 v[22:23], v[40:41], v[132:133] op_sel:[1,1] op_sel_hi:[0,1] neg_hi:[1,0]
	s_mov_b32 s36, s97
	v_pk_fma_f32 v[40:41], v[40:41], v[132:133], v[22:23] op_sel_hi:[1,0,1]
	v_pk_mul_f32 v[22:23], v[42:43], v[130:131] op_sel:[1,1] op_sel_hi:[0,1] neg_hi:[1,0]
	s_mov_b32 s37, s95
	v_pk_fma_f32 v[42:43], v[42:43], v[130:131], v[22:23] op_sel_hi:[1,0,1]
	v_pk_mul_f32 v[22:23], v[82:83], v[128:129] op_sel:[1,1] op_sel_hi:[0,1] neg_hi:[1,0]
	s_mov_b32 s96, s95
	v_pk_fma_f32 v[22:23], v[82:83], v[128:129], v[22:23] op_sel_hi:[1,0,1]
	v_pk_mul_f32 v[82:83], v[48:49], v[126:127] op_sel:[1,1] op_sel_hi:[0,1] neg_hi:[1,0]
	s_mov_b32 s23, s25
	v_pk_fma_f32 v[48:49], v[48:49], v[126:127], v[82:83] op_sel_hi:[1,0,1]
	v_pk_mul_f32 v[82:83], v[52:53], v[124:125] op_sel:[1,1] op_sel_hi:[0,1] neg_hi:[1,0]
	s_mov_b32 s22, s83
	v_pk_fma_f32 v[52:53], v[52:53], v[124:125], v[82:83] op_sel_hi:[1,0,1]
	v_pk_mul_f32 v[82:83], v[56:57], v[122:123] op_sel:[1,1] op_sel_hi:[0,1] neg_hi:[1,0]
	s_mov_b32 s26, s29
	v_pk_fma_f32 v[56:57], v[56:57], v[122:123], v[82:83] op_sel_hi:[1,0,1]
	v_pk_mul_f32 v[82:83], v[30:31], v[120:121] op_sel:[1,1] op_sel_hi:[0,1] neg_hi:[1,0]
	s_mov_b32 s27, s87
	v_pk_fma_f32 v[30:31], v[30:31], v[120:121], v[82:83] op_sel_hi:[1,0,1]
	v_pk_mul_f32 v[82:83], v[38:39], v[118:119] op_sel:[1,1] op_sel_hi:[0,1] neg_hi:[1,0]
	s_movk_i32 s39, 0x2000
	v_pk_fma_f32 v[38:39], v[38:39], v[118:119], v[82:83] op_sel_hi:[1,0,1]
	v_pk_mul_f32 v[82:83], v[64:65], v[116:117] op_sel:[1,1] op_sel_hi:[0,1] neg_hi:[1,0]
	s_mov_b32 s44, s94
	v_pk_fma_f32 v[64:65], v[64:65], v[116:117], v[82:83] op_sel_hi:[1,0,1]
	v_pk_mul_f32 v[82:83], v[66:67], v[114:115] op_sel:[1,1] op_sel_hi:[0,1] neg_hi:[1,0]
	v_mov_b32_e32 v118, v164
	v_pk_fma_f32 v[66:67], v[66:67], v[114:115], v[82:83] op_sel_hi:[1,0,1]
	v_pk_mul_f32 v[82:83], v[44:45], v[112:113] op_sel:[1,1] op_sel_hi:[0,1] neg_hi:[1,0]
	v_mov_b32_e32 v120, v166
	v_pk_fma_f32 v[44:45], v[44:45], v[112:113], v[82:83] op_sel_hi:[1,0,1]
	v_pk_mul_f32 v[82:83], v[46:47], v[110:111] op_sel:[1,1] op_sel_hi:[0,1] neg_hi:[1,0]
	v_mov_b32_e32 v122, v168
	v_pk_fma_f32 v[46:47], v[46:47], v[110:111], v[82:83] op_sel_hi:[1,0,1]
	v_pk_mul_f32 v[82:83], v[50:51], v[108:109] op_sel:[1,1] op_sel_hi:[0,1] neg_hi:[1,0]
	v_mov_b32_e32 v124, v170
	v_pk_fma_f32 v[50:51], v[50:51], v[108:109], v[82:83] op_sel_hi:[1,0,1]
	v_pk_mul_f32 v[82:83], v[54:55], v[106:107] op_sel:[1,1] op_sel_hi:[0,1] neg_hi:[1,0]
	s_movk_i32 s33, 0x5000
	v_pk_fma_f32 v[54:55], v[54:55], v[106:107], v[82:83] op_sel_hi:[1,0,1]
	v_pk_mul_f32 v[82:83], v[58:59], v[104:105] op_sel:[1,1] op_sel_hi:[0,1] neg_hi:[1,0]
	v_pk_fma_f32 v[58:59], v[58:59], v[104:105], v[82:83] op_sel_hi:[1,0,1]
	v_pk_mul_f32 v[82:83], v[60:61], v[102:103] op_sel:[1,1] op_sel_hi:[0,1] neg_hi:[1,0]
	v_pk_fma_f32 v[60:61], v[60:61], v[102:103], v[82:83] op_sel_hi:[1,0,1]
	v_pk_mul_f32 v[82:83], v[62:63], v[100:101] op_sel:[1,1] op_sel_hi:[0,1] neg_hi:[1,0]
	v_pk_fma_f32 v[62:63], v[62:63], v[100:101], v[82:83] op_sel_hi:[1,0,1]
	v_pk_mul_f32 v[82:83], v[24:25], v[98:99] op_sel:[1,1] op_sel_hi:[0,1] neg_hi:[1,0]
	v_pk_fma_f32 v[24:25], v[24:25], v[98:99], v[82:83] op_sel_hi:[1,0,1]
	v_pk_mul_f32 v[82:83], v[68:69], v[96:97] op_sel:[1,1] op_sel_hi:[0,1] neg_hi:[1,0]
	v_add_f32_e32 v22, v24, v22
	v_pk_fma_f32 v[68:69], v[68:69], v[96:97], v[82:83] op_sel_hi:[1,0,1]
	v_pk_mul_f32 v[82:83], v[70:71], v[94:95] op_sel:[1,1] op_sel_hi:[0,1] neg_hi:[1,0]
	v_add_f32_e32 v20, v17, v22
	v_pk_fma_f32 v[70:71], v[70:71], v[94:95], v[82:83] op_sel_hi:[1,0,1]
	v_pk_mul_f32 v[82:83], v[72:73], v[92:93] op_sel:[1,1] op_sel_hi:[0,1] neg_hi:[1,0]
	v_mov_b32_e32 v94, v170
	v_pk_fma_f32 v[72:73], v[72:73], v[92:93], v[82:83] op_sel_hi:[1,0,1]
	v_pk_mul_f32 v[82:83], v[74:75], v[90:91] op_sel:[1,1] op_sel_hi:[0,1] neg_hi:[1,0]
	v_mov_b32_e32 v92, v169
	v_pk_fma_f32 v[74:75], v[74:75], v[90:91], v[82:83] op_sel_hi:[1,0,1]
	v_pk_mul_f32 v[82:83], v[76:77], v[88:89] op_sel:[1,1] op_sel_hi:[0,1] neg_hi:[1,0]
	v_mov_b32_e32 v90, v168
	v_pk_fma_f32 v[76:77], v[76:77], v[88:89], v[82:83] op_sel_hi:[1,0,1]
	v_pk_mul_f32 v[82:83], v[78:79], v[86:87] op_sel:[1,1] op_sel_hi:[0,1] neg_hi:[1,0]
	v_mov_b32_e32 v88, v167
	v_pk_fma_f32 v[78:79], v[78:79], v[86:87], v[82:83] op_sel_hi:[1,0,1]
	v_pk_mul_f32 v[82:83], v[84:85], v[80:81] op_sel:[1,1] op_sel_hi:[1,0] neg_hi:[0,1]
	v_mov_b32_e32 v86, v166
	v_pk_fma_f32 v[80:81], v[80:81], v[84:85], v[82:83] op_sel_hi:[1,0,1]
	v_mov_b32_e32 v84, v165
	v_pk_add_f32 v[96:97], v[80:81], v[66:67]
	v_pk_add_f32 v[66:67], v[80:81], v[66:67] neg_lo:[0,1] neg_hi:[0,1]
	s_nop 0
	v_sub_f32_e32 v82, v25, v23
	v_pk_mul_f32 v[80:81], v[94:95], v[66:67] op_sel:[0,1] op_sel_hi:[0,0] neg_lo:[0,1]
	v_pk_fma_f32 v[80:81], v[10:11], v[66:67], v[80:81] op_sel_hi:[0,1,1]
	v_pk_add_f32 v[66:67], v[78:79], v[64:65]
	v_pk_add_f32 v[64:65], v[78:79], v[64:65] neg_lo:[0,1] neg_hi:[0,1]
	v_pk_mul_f32 v[78:79], v[92:93], v[64:65] op_sel:[0,1] op_sel_hi:[0,0] neg_lo:[0,1]
	v_pk_fma_f32 v[64:65], v[84:85], v[64:65], v[78:79] op_sel_hi:[0,1,1]
	v_pk_add_f32 v[78:79], v[76:77], v[38:39]
	v_pk_add_f32 v[38:39], v[76:77], v[38:39] neg_lo:[0,1] neg_hi:[0,1]
	s_barrier
	v_pk_mul_f32 v[76:77], v[90:91], v[38:39] op_sel:[0,1] op_sel_hi:[0,0] neg_lo:[0,1]
	v_pk_fma_f32 v[76:77], v[86:87], v[38:39], v[76:77] op_sel_hi:[0,1,1]
	v_pk_add_f32 v[38:39], v[74:75], v[30:31]
	v_pk_add_f32 v[30:31], v[74:75], v[30:31] neg_lo:[0,1] neg_hi:[0,1]
	v_pk_mul_f32 v[74:75], v[88:89], v[30:31] op_sel:[0,1] op_sel_hi:[0,0] neg_lo:[0,1]
	v_pk_fma_f32 v[30:31], v[88:89], v[30:31], v[74:75] op_sel_hi:[0,1,1]
	v_pk_add_f32 v[74:75], v[72:73], v[56:57]
	v_pk_add_f32 v[56:57], v[72:73], v[56:57] neg_lo:[0,1] neg_hi:[0,1]
	v_sub_f32_e32 v22, v17, v22
	v_pk_mul_f32 v[72:73], v[86:87], v[56:57] op_sel:[0,1] op_sel_hi:[0,0] neg_lo:[0,1]
	v_pk_fma_f32 v[72:73], v[90:91], v[56:57], v[72:73] op_sel_hi:[0,1,1]
	v_pk_add_f32 v[56:57], v[70:71], v[52:53]
	v_pk_add_f32 v[52:53], v[70:71], v[52:53] neg_lo:[0,1] neg_hi:[0,1]
	v_ashrrev_i32_e32 v15, 31, v14
	v_pk_mul_f32 v[70:71], v[84:85], v[52:53] op_sel:[0,1] op_sel_hi:[0,0] neg_lo:[0,1]
	v_pk_fma_f32 v[52:53], v[92:93], v[52:53], v[70:71] op_sel_hi:[0,1,1]
	v_pk_add_f32 v[70:71], v[68:69], v[48:49]
	v_pk_add_f32 v[48:49], v[68:69], v[48:49] neg_lo:[0,1] neg_hi:[0,1]
	v_lshl_add_u64 v[14:15], v[14:15], 2, s[70:71]
	v_pk_mul_f32 v[68:69], v[10:11], v[48:49] op_sel:[0,1] op_sel_hi:[0,0] neg_lo:[0,1]
	v_pk_fma_f32 v[98:99], v[94:95], v[48:49], v[68:69] op_sel_hi:[0,1,1]
	v_pk_add_f32 v[48:49], v[62:63], v[42:43]
	v_pk_add_f32 v[42:43], v[62:63], v[42:43] neg_lo:[0,1] neg_hi:[0,1]
	v_pk_mul_f32 v[62:63], v[10:11], v[42:43] op_sel:[0,1] op_sel_hi:[0,0] neg_lo:[0,1]
	v_pk_fma_f32 v[62:63], v[94:95], v[42:43], v[62:63] op_sel_hi:[0,1,1] neg_lo:[1,0,0] neg_hi:[1,0,0]
	v_pk_add_f32 v[42:43], v[60:61], v[40:41]
	v_pk_add_f32 v[40:41], v[60:61], v[40:41] neg_lo:[0,1] neg_hi:[0,1]
	v_pk_mul_f32 v[60:61], v[84:85], v[40:41] op_sel:[0,1] op_sel_hi:[0,0] neg_lo:[0,1]
	v_pk_fma_f32 v[100:101], v[92:93], v[40:41], v[60:61] op_sel_hi:[0,1,1] neg_lo:[1,0,0] neg_hi:[1,0,0]
	v_pk_add_f32 v[60:61], v[58:59], v[36:37]
	v_pk_add_f32 v[36:37], v[58:59], v[36:37] neg_lo:[0,1] neg_hi:[0,1]
	v_pk_mul_f32 v[40:41], v[86:87], v[36:37] op_sel:[0,1] op_sel_hi:[0,0] neg_lo:[0,1]
	v_pk_fma_f32 v[58:59], v[90:91], v[36:37], v[40:41] op_sel_hi:[0,1,1] neg_lo:[1,0,0] neg_hi:[1,0,0]
	v_pk_add_f32 v[40:41], v[54:55], v[34:35]
	v_pk_add_f32 v[34:35], v[54:55], v[34:35] neg_lo:[0,1] neg_hi:[0,1]
	v_pk_add_f32 v[54:55], v[46:47], v[28:29]
	v_pk_mul_f32 v[36:37], v[88:89], v[34:35] op_sel:[0,1] op_sel_hi:[0,0] neg_lo:[0,1]
	v_pk_fma_f32 v[34:35], v[88:89], v[34:35], v[36:37] op_sel_hi:[0,1,1] neg_lo:[1,0,0] neg_hi:[1,0,0]
	v_pk_add_f32 v[36:37], v[50:51], v[32:33]
	v_pk_add_f32 v[32:33], v[50:51], v[32:33] neg_lo:[0,1] neg_hi:[0,1]
	v_pk_add_f32 v[28:29], v[46:47], v[28:29] neg_lo:[0,1] neg_hi:[0,1]
	v_pk_mul_f32 v[50:51], v[90:91], v[32:33] op_sel:[0,1] op_sel_hi:[0,0] neg_lo:[0,1]
	v_pk_fma_f32 v[86:87], v[86:87], v[32:33], v[50:51] op_sel_hi:[0,1,1] neg_lo:[1,0,0] neg_hi:[1,0,0]
	v_pk_mul_f32 v[32:33], v[92:93], v[28:29] op_sel:[0,1] op_sel_hi:[0,0] neg_lo:[0,1]
	v_pk_fma_f32 v[46:47], v[84:85], v[28:29], v[32:33] op_sel_hi:[0,1,1] neg_lo:[1,0,0] neg_hi:[1,0,0]
	v_pk_add_f32 v[28:29], v[44:45], v[26:27]
	v_pk_add_f32 v[26:27], v[44:45], v[26:27] neg_lo:[0,1] neg_hi:[0,1]
	v_pk_add_f32 v[50:51], v[66:67], v[42:43]
	v_pk_mul_f32 v[32:33], v[94:95], v[26:27] op_sel:[0,1] op_sel_hi:[0,0] neg_lo:[0,1]
	v_pk_fma_f32 v[90:91], v[10:11], v[26:27], v[32:33] op_sel_hi:[0,1,1] neg_lo:[1,0,0] neg_hi:[1,0,0]
	v_pk_add_f32 v[32:33], v[96:97], v[48:49] neg_lo:[0,1] neg_hi:[0,1]
	v_pk_add_f32 v[26:27], v[96:97], v[48:49]
	v_pk_mul_f32 v[44:45], v[92:93], v[32:33] op_sel:[0,1] op_sel_hi:[0,0] neg_lo:[0,1]
	v_pk_fma_f32 v[48:49], v[84:85], v[32:33], v[44:45] op_sel_hi:[0,1,1]
	v_pk_add_f32 v[32:33], v[66:67], v[42:43] neg_lo:[0,1] neg_hi:[0,1]
	v_pk_add_f32 v[44:45], v[78:79], v[60:61] neg_lo:[0,1] neg_hi:[0,1]
	v_pk_mul_f32 v[42:43], v[88:89], v[32:33] op_sel:[0,1] op_sel_hi:[0,0] neg_lo:[0,1]
	v_pk_fma_f32 v[32:33], v[88:89], v[32:33], v[42:43] op_sel_hi:[0,1,1]
	v_pk_add_f32 v[42:43], v[78:79], v[60:61]
	v_pk_mul_f32 v[60:61], v[84:85], v[44:45] op_sel:[0,1] op_sel_hi:[0,0] neg_lo:[0,1]
	v_pk_add_f32 v[78:79], v[74:75], v[36:37]
	v_pk_add_f32 v[36:37], v[74:75], v[36:37] neg_lo:[0,1] neg_hi:[0,1]
	v_pk_fma_f32 v[68:69], v[92:93], v[44:45], v[60:61] op_sel_hi:[0,1,1]
	v_pk_mul_f32 v[44:45], v[84:85], v[36:37] op_sel:[0,1] op_sel_hi:[0,0] neg_lo:[0,1]
	v_pk_fma_f32 v[74:75], v[92:93], v[36:37], v[44:45] op_sel_hi:[0,1,1] neg_lo:[1,0,0] neg_hi:[1,0,0]
	v_pk_add_f32 v[36:37], v[56:57], v[54:55] neg_lo:[0,1] neg_hi:[0,1]
	v_pk_add_f32 v[60:61], v[56:57], v[54:55]
	v_pk_mul_f32 v[44:45], v[88:89], v[36:37] op_sel:[0,1] op_sel_hi:[0,0] neg_lo:[0,1]
	v_pk_fma_f32 v[44:45], v[88:89], v[36:37], v[44:45] op_sel_hi:[0,1,1] neg_lo:[1,0,0] neg_hi:[1,0,0]
	v_pk_add_f32 v[36:37], v[70:71], v[28:29]
	v_pk_add_f32 v[28:29], v[70:71], v[28:29] neg_lo:[0,1] neg_hi:[0,1]
	v_pk_add_f32 v[66:67], v[26:27], v[78:79]
	v_pk_mul_f32 v[54:55], v[92:93], v[28:29] op_sel:[0,1] op_sel_hi:[0,0] neg_lo:[0,1]
	v_pk_add_f32 v[26:27], v[26:27], v[78:79] neg_lo:[0,1] neg_hi:[0,1]
	v_pk_fma_f32 v[94:95], v[84:85], v[28:29], v[54:55] op_sel_hi:[0,1,1] neg_lo:[1,0,0] neg_hi:[1,0,0]
	v_pk_mul_f32 v[28:29], v[88:89], v[26:27] op_sel:[0,1] op_sel_hi:[0,0] neg_lo:[0,1]
	v_pk_fma_f32 v[26:27], v[88:89], v[26:27], v[28:29] op_sel_hi:[0,1,1]
	v_pk_add_f32 v[28:29], v[42:43], v[36:37] neg_lo:[0,1] neg_hi:[0,1]
	v_pk_add_f32 v[70:71], v[42:43], v[36:37]
	v_pk_mul_f32 v[36:37], v[88:89], v[28:29] op_sel:[0,1] op_sel_hi:[0,0] neg_lo:[0,1]
	v_pk_fma_f32 v[36:37], v[88:89], v[28:29], v[36:37] op_sel_hi:[0,1,1] neg_lo:[1,0,0] neg_hi:[1,0,0]
	v_pk_add_f32 v[28:29], v[48:49], v[74:75] neg_lo:[0,1] neg_hi:[0,1]
	v_pk_add_f32 v[54:55], v[48:49], v[74:75]
	v_pk_mul_f32 v[42:43], v[88:89], v[28:29] op_sel:[0,1] op_sel_hi:[0,0] neg_lo:[0,1]
	v_pk_fma_f32 v[28:29], v[88:89], v[28:29], v[42:43] op_sel_hi:[0,1,1]
	v_pk_add_f32 v[42:43], v[68:69], v[94:95] neg_lo:[0,1] neg_hi:[0,1]
	v_pk_add_f32 v[74:75], v[80:81], v[62:63]
	v_pk_mul_f32 v[48:49], v[88:89], v[42:43] op_sel:[0,1] op_sel_hi:[0,0] neg_lo:[0,1]
	v_pk_fma_f32 v[42:43], v[88:89], v[42:43], v[48:49] op_sel_hi:[0,1,1] neg_lo:[1,0,0] neg_hi:[1,0,0]
	v_pk_add_f32 v[48:49], v[80:81], v[62:63] neg_lo:[0,1] neg_hi:[0,1]
	v_pk_add_f32 v[56:57], v[68:69], v[94:95]
	v_pk_mul_f32 v[62:63], v[92:93], v[48:49] op_sel:[0,1] op_sel_hi:[0,0] neg_lo:[0,1]
	v_pk_fma_f32 v[94:95], v[84:85], v[48:49], v[62:63] op_sel_hi:[0,1,1]
	v_pk_add_f32 v[48:49], v[64:65], v[100:101] neg_lo:[0,1] neg_hi:[0,1]
	v_pk_add_f32 v[68:69], v[64:65], v[100:101]
	v_pk_mul_f32 v[62:63], v[88:89], v[48:49] op_sel:[0,1] op_sel_hi:[0,0] neg_lo:[0,1]
	v_pk_add_f32 v[64:65], v[76:77], v[58:59]
	v_pk_add_f32 v[58:59], v[76:77], v[58:59] neg_lo:[0,1] neg_hi:[0,1]
	v_pk_fma_f32 v[48:49], v[88:89], v[48:49], v[62:63] op_sel_hi:[0,1,1]
	v_pk_mul_f32 v[62:63], v[84:85], v[58:59] op_sel:[0,1] op_sel_hi:[0,0] neg_lo:[0,1]
	v_pk_fma_f32 v[96:97], v[92:93], v[58:59], v[62:63] op_sel_hi:[0,1,1]
	v_pk_add_f32 v[58:59], v[72:73], v[86:87] neg_lo:[0,1] neg_hi:[0,1]
	v_pk_add_f32 v[76:77], v[52:53], v[46:47]
	v_pk_add_f32 v[46:47], v[52:53], v[46:47] neg_lo:[0,1] neg_hi:[0,1]
	v_pk_add_f32 v[62:63], v[72:73], v[86:87]
	v_pk_mul_f32 v[72:73], v[84:85], v[58:59] op_sel:[0,1] op_sel_hi:[0,0] neg_lo:[0,1]
	v_pk_mul_f32 v[52:53], v[88:89], v[46:47] op_sel:[0,1] op_sel_hi:[0,0] neg_lo:[0,1]
	v_pk_fma_f32 v[86:87], v[92:93], v[58:59], v[72:73] op_sel_hi:[0,1,1] neg_lo:[1,0,0] neg_hi:[1,0,0]
	v_pk_fma_f32 v[58:59], v[88:89], v[46:47], v[52:53] op_sel_hi:[0,1,1] neg_lo:[1,0,0] neg_hi:[1,0,0]
	v_pk_add_f32 v[46:47], v[98:99], v[90:91]
	v_pk_add_f32 v[52:53], v[98:99], v[90:91] neg_lo:[0,1] neg_hi:[0,1]
	v_pk_add_f32 v[80:81], v[64:65], v[46:47]
	v_pk_add_f32 v[46:47], v[64:65], v[46:47] neg_lo:[0,1] neg_hi:[0,1]
	v_pk_mul_f32 v[64:65], v[88:89], v[46:47] op_sel:[0,1] op_sel_hi:[0,0] neg_lo:[0,1]
	v_pk_fma_f32 v[64:65], v[88:89], v[46:47], v[64:65] op_sel_hi:[0,1,1] neg_lo:[1,0,0] neg_hi:[1,0,0]
	v_pk_add_f32 v[46:47], v[94:95], v[86:87] neg_lo:[0,1] neg_hi:[0,1]
	v_pk_mul_f32 v[72:73], v[92:93], v[52:53] op_sel:[0,1] op_sel_hi:[0,0] neg_lo:[0,1]
	v_pk_add_f32 v[78:79], v[74:75], v[62:63]
	v_pk_add_f32 v[62:63], v[74:75], v[62:63] neg_lo:[0,1] neg_hi:[0,1]
	v_pk_fma_f32 v[52:53], v[84:85], v[52:53], v[72:73] op_sel_hi:[0,1,1] neg_lo:[1,0,0] neg_hi:[1,0,0]
	v_pk_mul_f32 v[74:75], v[88:89], v[46:47] op_sel:[0,1] op_sel_hi:[0,0] neg_lo:[0,1]
	v_pk_fma_f32 v[46:47], v[88:89], v[46:47], v[74:75] op_sel_hi:[0,1,1]
	v_pk_add_f32 v[74:75], v[96:97], v[52:53]
	v_pk_add_f32 v[52:53], v[96:97], v[52:53] neg_lo:[0,1] neg_hi:[0,1]
	v_add_f32_e32 v30, v30, v34
	v_pk_mul_f32 v[84:85], v[88:89], v[52:53] op_sel:[0,1] op_sel_hi:[0,0] neg_lo:[0,1]
	v_sub_f32_e32 v34, v16, v18
	v_sub_f32_e32 v13, v51, v61
	v_pk_fma_f32 v[52:53], v[88:89], v[52:53], v[84:85] op_sel_hi:[0,1,1] neg_lo:[1,0,0] neg_hi:[1,0,0]
	v_sub_f32_e32 v51, v34, v82
	v_sub_f32_e32 v25, v29, v43
	v_sub_f32_e32 v43, v31, v35
	v_sub_f32_e32 v35, v49, v59
	v_sub_f32_e32 v10, v47, v53
	v_add_f32_e32 v49, v50, v60
	v_add_f32_e32 v50, v68, v76
	v_add_f32_e32 v53, v51, v30
	v_sub_f32_e32 v23, v27, v37
	v_sub_f32_e32 v27, v55, v57
	v_add_f32_e32 v38, v38, v40
	v_add_f32_e32 v40, v78, v80
	v_add_f32_e32 v55, v53, v50
	v_add_f32_e32 v16, v55, v40
	v_sub_f32_e32 v41, v39, v41
	v_add_f32_e32 v21, v20, v38
	global_store_dword v[14:15], v16, off offset:2048
	v_add_co_u32_e32 v16, vcc, s10, v14
	v_add_f32_e32 v47, v66, v70
	v_add_f32_e32 v24, v21, v49
	v_add_f32_e32 v32, v32, v44
	v_sub_f32_e32 v44, v22, v41
	v_addc_co_u32_e32 v17, vcc, 0, v15, vcc
	v_pk_mul_f32 v[72:73], v[88:89], v[62:63] op_sel:[0,1] op_sel_hi:[0,0] neg_lo:[0,1]
	v_add_f32_e32 v19, v24, v47
	v_add_f32_e32 v54, v54, v56
	v_add_f32_e32 v56, v44, v32
	v_add_co_u32_e32 v18, vcc, s11, v14
	v_add_f32_e32 v34, v34, v82
	v_pk_fma_f32 v[62:63], v[88:89], v[62:63], v[72:73] op_sel_hi:[0,1,1]
	v_pk_add_f32 v[72:73], v[94:95], v[86:87]
	global_store_dword v[14:15], v19, off
	v_add_f32_e32 v57, v56, v54
	v_addc_co_u32_e32 v19, vcc, 0, v15, vcc
	v_add_f32_e32 v48, v48, v58
	v_sub_f32_e32 v58, v34, v43
	global_store_dword v[18:19], v57, off offset:-4096
	v_add_f32_e32 v57, v72, v74
	v_add_f32_e32 v59, v58, v48
	v_sub_f32_e32 v20, v20, v38
	v_sub_f32_e32 v37, v33, v45
	v_sub_f32_e32 v45, v69, v77
	v_add_f32_e32 v60, v59, v57
	v_add_f32_e32 v26, v26, v36
	v_sub_f32_e32 v36, v20, v13
	v_sub_f32_e32 v30, v51, v30
	global_store_dword v[16:17], v60, off offset:2048
	v_add_f32_e32 v16, v36, v26
	v_add_f32_e32 v38, v62, v64
	v_sub_f32_e32 v51, v30, v45
	global_store_dword v[18:19], v16, off
	v_add_f32_e32 v16, v51, v38
	global_store_dword v[18:19], v16, off offset:2048
	v_add_co_u32_e32 v16, vcc, s78, v14
	v_add_f32_e32 v22, v22, v41
	s_nop 0
	v_addc_co_u32_e32 v17, vcc, 0, v15, vcc
	v_add_f32_e32 v28, v28, v42
	v_sub_f32_e32 v41, v22, v37
	v_add_co_u32_e32 v18, vcc, s43, v14
	v_add_f32_e32 v42, v41, v28
	s_nop 0
	v_addc_co_u32_e32 v19, vcc, 0, v15, vcc
	v_add_f32_e32 v34, v34, v43
	global_store_dword v[18:19], v42, off offset:-4096
	v_add_f32_e32 v42, v46, v52
	v_sub_f32_e32 v43, v34, v35
	v_sub_f32_e32 v39, v67, v71
	v_add_f32_e32 v46, v43, v42
	v_sub_f32_e32 v21, v21, v49
	v_sub_f32_e32 v33, v79, v81
	global_store_dword v[16:17], v46, off offset:2048
	v_sub_f32_e32 v16, v21, v39
	v_sub_f32_e32 v46, v53, v50
	global_store_dword v[18:19], v16, off
	v_sub_f32_e32 v16, v46, v33
	global_store_dword v[18:19], v16, off offset:2048
	v_add_co_u32_e32 v16, vcc, s13, v14
	v_sub_f32_e32 v32, v44, v32
	s_nop 0
	v_addc_co_u32_e32 v17, vcc, 0, v15, vcc
	v_add_co_u32_e32 v18, vcc, s12, v14
	v_sub_f32_e32 v44, v32, v27
	s_nop 0
	v_addc_co_u32_e32 v19, vcc, 0, v15, vcc
	v_sub_f32_e32 v31, v73, v75
	global_store_dword v[18:19], v44, off offset:-4096
	v_sub_f32_e32 v44, v58, v48
	v_sub_f32_e32 v48, v44, v31
	v_add_f32_e32 v20, v20, v13
	v_sub_f32_e32 v29, v63, v65
	global_store_dword v[16:17], v48, off offset:2048
	v_sub_f32_e32 v13, v20, v23
	v_add_f32_e32 v30, v30, v45
	v_add_co_u32_e32 v16, vcc, s16, v14
	global_store_dword v[18:19], v13, off
	v_sub_f32_e32 v13, v30, v29
	v_addc_co_u32_e32 v17, vcc, 0, v15, vcc
	global_store_dword v[18:19], v13, off offset:2048
	v_add_f32_e32 v22, v22, v37
	v_add_co_u32_e32 v18, vcc, s8, v14
	v_sub_f32_e32 v13, v22, v25
	s_nop 0
	v_addc_co_u32_e32 v19, vcc, 0, v15, vcc
	global_store_dword v[18:19], v13, off offset:-4096
	v_add_f32_e32 v13, v34, v35
	v_sub_f32_e32 v34, v13, v10
	global_store_dword v[16:17], v34, off offset:2048
	v_sub_f32_e32 v16, v24, v47
	global_store_dword v[18:19], v16, off
	v_sub_f32_e32 v16, v55, v40
	global_store_dword v[18:19], v16, off offset:2048
	v_add_co_u32_e32 v16, vcc, s9, v14
	v_sub_f32_e32 v24, v56, v54
	s_nop 0
	v_addc_co_u32_e32 v17, vcc, 0, v15, vcc
	v_add_co_u32_e32 v18, vcc, s7, v14
	v_add_f32_e32 v10, v13, v10
	s_nop 0
	v_addc_co_u32_e32 v19, vcc, 0, v15, vcc
	global_store_dword v[18:19], v24, off offset:-4096
	v_sub_f32_e32 v24, v59, v57
	global_store_dword v[16:17], v24, off offset:2048
	v_sub_f32_e32 v16, v36, v26
	global_store_dword v[18:19], v16, off
	v_sub_f32_e32 v16, v51, v38
	global_store_dword v[18:19], v16, off offset:2048
	v_add_co_u32_e32 v16, vcc, s5, v14
	v_sub_f32_e32 v24, v41, v28
	s_nop 0
	v_addc_co_u32_e32 v17, vcc, 0, v15, vcc
	v_add_co_u32_e32 v18, vcc, s6, v14
	s_nop 1
	v_addc_co_u32_e32 v19, vcc, 0, v15, vcc
	global_store_dword v[18:19], v24, off offset:-4096
	v_sub_f32_e32 v24, v43, v42
	global_store_dword v[16:17], v24, off offset:2048
	v_add_f32_e32 v16, v21, v39
	global_store_dword v[18:19], v16, off
	v_add_f32_e32 v16, v46, v33
	global_store_dword v[18:19], v16, off offset:2048
	v_add_co_u32_e32 v16, vcc, s4, v14
	v_add_f32_e32 v21, v32, v27
	s_nop 0
	v_addc_co_u32_e32 v17, vcc, 0, v15, vcc
	v_add_co_u32_e32 v18, vcc, s1, v14
	s_nop 1
	v_addc_co_u32_e32 v19, vcc, 0, v15, vcc
	global_store_dword v[18:19], v21, off offset:-4096
	v_add_f32_e32 v21, v44, v31
	global_store_dword v[16:17], v21, off offset:2048
	v_add_f32_e32 v16, v20, v23
	global_store_dword v[18:19], v16, off
	v_add_f32_e32 v16, v30, v29
	v_add_co_u32_e32 v14, vcc, s0, v14
	global_store_dword v[18:19], v16, off offset:2048
	v_add_f32_e32 v16, v22, v25
	v_addc_co_u32_e32 v15, vcc, 0, v15, vcc
	global_store_dword v[14:15], v16, off
	global_store_dword v[14:15], v10, off offset:2048
	v_mov_b32_e32 v10, v183
	v_mov_b32_e32 v14, v184
	v_mov_b32_e32 v18, v182
	s_movk_i32 s0, 0xfe00
	v_sub_u32_e32 v13, 0x4000, v18
	v_cmp_eq_u32_e32 vcc, 0, v18
	v_cmp_eq_u32_e64 s[0:1], s0, v18
	v_cmp_eq_u32_e64 s[4:5], s48, v18
	v_cndmask_b32_e64 v20, v13, 0, vcc
	v_sub_u32_e32 v13, 0x3e00, v18
	v_cndmask_b32_e64 v22, v13, 0, s[0:1]
	v_sub_u32_e32 v13, 0x3c00, v18
	v_ashrrev_i32_e32 v21, 31, v20
	v_ashrrev_i32_e32 v23, 31, v22
	v_cndmask_b32_e64 v24, v13, 0, s[4:5]
	v_lshl_add_u64 v[20:21], v[20:21], 1, s[2:3]
	v_lshl_add_u64 v[22:23], v[22:23], 1, s[2:3]
	v_ashrrev_i32_e32 v25, 31, v24
	v_sub_u32_e32 v13, 0x3a00, v18
	v_cmp_eq_u32_e64 s[6:7], s49, v18
	v_lshl_add_u64 v[24:25], v[24:25], 1, s[2:3]
	global_load_ushort v15, v[20:21], off
	s_nop 0
	global_load_ushort v22, v[22:23], off
	s_nop 0
	global_load_ushort v23, v[24:25], off
	v_cndmask_b32_e64 v20, v13, 0, s[6:7]
	v_ashrrev_i32_e32 v21, 31, v20
	v_ashrrev_i32_e32 v19, 31, v18
	v_lshl_add_u64 v[20:21], v[20:21], 1, s[2:3]
	v_lshl_add_u64 v[16:17], v[18:19], 1, s[76:77]
	global_load_ushort v20, v[20:21], off
	s_nop 0
	global_load_ushort v13, v[16:17], off offset:3072
	v_sub_u32_e32 v24, 0x3800, v18
	v_sub_u32_e32 v26, 0x3600, v18
	v_sub_u32_e32 v28, 0x3400, v18
	v_sub_u32_e32 v32, 0x3200, v18
	v_cmp_eq_u32_e64 s[8:9], s59, v18
	s_mov_b32 s48, s21
	s_mov_b32 s49, s20
	s_mov_b32 s59, s82
	s_waitcnt vmcnt(4)
	v_lshlrev_b32_e32 v15, 16, v15
	v_cndmask_b32_e64 v19, -v15, v15, vcc
	s_waitcnt vmcnt(3)
	v_lshlrev_b32_e32 v15, 16, v22
	v_cndmask_b32_e64 v31, -v15, v15, s[0:1]
	s_waitcnt vmcnt(2)
	v_lshlrev_b32_e32 v15, 16, v23
	v_cndmask_b32_e64 v30, -v15, v15, s[4:5]
	v_cmp_eq_u32_e64 s[4:5], s51, v18
	s_waitcnt vmcnt(1)
	v_lshlrev_b32_e32 v15, 16, v20
	v_add_co_u32_e32 v20, vcc, s10, v16
	v_cndmask_b32_e64 v15, -v15, v15, s[6:7]
	s_nop 0
	v_addc_co_u32_e32 v21, vcc, 0, v17, vcc
	v_add_co_u32_e32 v22, vcc, s11, v16
	v_cmp_eq_u32_e64 s[6:7], s50, v18
	s_nop 0
	v_addc_co_u32_e32 v23, vcc, 0, v17, vcc
	v_cmp_eq_u32_e64 s[0:1], s57, v18
	v_cndmask_b32_e64 v24, v24, 0, s[6:7]
	v_cndmask_b32_e64 v26, v26, 0, s[4:5]
	v_cndmask_b32_e64 v28, v28, 0, s[0:1]
	v_cmp_eq_u32_e32 vcc, s58, v18
	v_ashrrev_i32_e32 v25, 31, v24
	v_ashrrev_i32_e32 v27, 31, v26
	v_ashrrev_i32_e32 v29, 31, v28
	v_cndmask_b32_e64 v32, v32, 0, vcc
	v_lshl_add_u64 v[24:25], v[24:25], 1, s[2:3]
	v_lshl_add_u64 v[26:27], v[26:27], 1, s[2:3]
	v_lshl_add_u64 v[28:29], v[28:29], 1, s[2:3]
	v_ashrrev_i32_e32 v33, 31, v32
	v_lshl_add_u64 v[32:33], v[32:33], 1, s[2:3]
	global_load_ushort v34, v[24:25], off
	s_nop 0
	global_load_ushort v26, v[26:27], off
	s_nop 0
	global_load_ushort v27, v[28:29], off
	s_nop 0
	global_load_ushort v28, v[32:33], off
	v_sub_u32_e32 v24, 0x3000, v18
	v_cndmask_b32_e64 v24, v24, 0, s[8:9]
	v_ashrrev_i32_e32 v25, 31, v24
	v_lshl_add_u64 v[24:25], v[24:25], 1, s[2:3]
	global_load_ushort v24, v[24:25], off
	s_nop 0
	global_load_ushort v32, v[20:21], off offset:3072
	v_cmp_eq_u32_e64 s[10:11], s79, v18
	s_mov_b32 s79, s80
	s_waitcnt vmcnt(6)
	v_lshlrev_b32_e32 v13, 16, v13
	s_mov_b32 s57, s18
	s_mov_b32 s58, s83
	s_waitcnt vmcnt(5)
	v_lshlrev_b32_e32 v25, 16, v34
	v_cndmask_b32_e64 v33, -v25, v25, s[6:7]
	s_waitcnt vmcnt(4)
	v_lshlrev_b32_e32 v25, 16, v26
	v_cndmask_b32_e64 v34, -v25, v25, s[4:5]
	s_waitcnt vmcnt(3)
	v_lshlrev_b32_e32 v25, 16, v27
	v_cndmask_b32_e64 v35, -v25, v25, s[0:1]
	v_add_co_u32_e64 v26, s[0:1], s78, v16
	s_waitcnt vmcnt(2)
	v_lshlrev_b32_e32 v25, 16, v28
	s_waitcnt vmcnt(1)
	v_lshlrev_b32_e32 v24, 16, v24
	v_addc_co_u32_e64 v27, s[0:1], 0, v17, s[0:1]
	v_cndmask_b32_e64 v36, -v25, v25, vcc
	v_cndmask_b32_e64 v37, -v24, v24, s[8:9]
	v_sub_u32_e32 v24, 0x2e00, v18
	v_cmp_eq_u32_e32 vcc, s60, v18
	v_sub_u32_e32 v28, 0x2c00, v18
	v_cmp_eq_u32_e64 s[0:1], s61, v18
	v_cndmask_b32_e64 v24, v24, 0, vcc
	v_ashrrev_i32_e32 v25, 31, v24
	v_cndmask_b32_e64 v28, v28, 0, s[0:1]
	v_ashrrev_i32_e32 v29, 31, v28
	v_lshl_add_u64 v[24:25], v[24:25], 1, s[2:3]
	v_lshl_add_u64 v[28:29], v[28:29], 1, s[2:3]
	global_load_ushort v41, v[24:25], off
	s_nop 0
	global_load_ushort v28, v[28:29], off
	v_sub_u32_e32 v24, 0x2a00, v18
	v_cmp_eq_u32_e64 s[4:5], s62, v18
	v_cmp_eq_u32_e64 s[6:7], s63, v18
	v_cmp_eq_u32_e64 s[8:9], s68, v18
	v_cndmask_b32_e64 v24, v24, 0, s[4:5]
	v_ashrrev_i32_e32 v25, 31, v24
	v_lshl_add_u64 v[24:25], v[24:25], 1, s[2:3]
	global_load_ushort v29, v[24:25], off
	v_sub_u32_e32 v24, 0x2800, v18
	v_cndmask_b32_e64 v24, v24, 0, s[6:7]
	v_ashrrev_i32_e32 v25, 31, v24
	v_lshl_add_u64 v[24:25], v[24:25], 1, s[2:3]
	global_load_ushort v38, v[26:27], off offset:1024
	global_load_ushort v40, v[26:27], off offset:2048
	global_load_ushort v39, v[26:27], off offset:3072
	global_load_ushort v44, v[24:25], off
	v_sub_u32_e32 v26, 0x2600, v18
	s_mov_b32 s78, s81
	s_mov_b32 s60, s87
	s_mov_b32 s61, s86
	s_mov_b32 s68, s89
	s_mov_b32 s62, s93
	s_mov_b32 s63, s92
	s_waitcnt vmcnt(6)
	v_lshlrev_b32_e32 v24, 16, v41
	v_cndmask_b32_e64 v43, -v24, v24, vcc
	s_waitcnt vmcnt(5)
	v_lshlrev_b32_e32 v24, 16, v28
	v_cndmask_b32_e64 v41, -v24, v24, s[0:1]
	v_add_co_u32_e64 v28, s[0:1], s13, v16
	s_waitcnt vmcnt(4)
	v_lshlrev_b32_e32 v24, 16, v29
	v_cndmask_b32_e64 v42, -v24, v24, s[4:5]
	v_add_co_u32_e32 v24, vcc, s43, v16
	v_addc_co_u32_e64 v29, s[0:1], 0, v17, s[0:1]
	s_nop 0
	v_addc_co_u32_e32 v25, vcc, 0, v17, vcc
	v_cmp_eq_u32_e32 vcc, s66, v18
	v_cmp_eq_u32_e64 s[4:5], s74, v18
	v_cmp_eq_u32_e64 s[0:1], s75, v18
	v_cndmask_b32_e64 v26, v26, 0, vcc
	v_ashrrev_i32_e32 v27, 31, v26
	v_lshl_add_u64 v[26:27], v[26:27], 1, s[2:3]
	global_load_ushort v26, v[26:27], off
	s_waitcnt vmcnt(1)
	v_lshlrev_b32_e32 v27, 16, v44
	v_sub_u32_e32 v44, 0x2200, v18
	v_cndmask_b32_e64 v45, -v27, v27, s[6:7]
	v_cndmask_b32_e64 v46, v44, 0, s[8:9]
	v_sub_u32_e32 v44, 0x2000, v18
	v_cmp_eq_u32_e64 s[6:7], s69, v18
	v_ashrrev_i32_e32 v47, 31, v46
	v_lshl_add_u64 v[46:47], v[46:47], 1, s[2:3]
	v_cndmask_b32_e64 v50, v44, 0, s[6:7]
	v_sub_u32_e32 v44, 0x1e00, v18
	v_cndmask_b32_e64 v52, v44, 0, s[4:5]
	v_sub_u32_e32 v44, 0x1c00, v18
	v_ashrrev_i32_e32 v51, 31, v50
	v_cndmask_b32_e64 v54, v44, 0, s[0:1]
	v_lshl_add_u64 v[50:51], v[50:51], 1, s[2:3]
	v_ashrrev_i32_e32 v53, 31, v52
	v_ashrrev_i32_e32 v55, 31, v54
	v_lshl_add_u64 v[52:53], v[52:53], 1, s[2:3]
	v_lshl_add_u64 v[54:55], v[54:55], 1, s[2:3]
	s_mov_b32 s66, s25
	s_mov_b32 s69, s88
	s_mov_b32 s74, s29
	s_mov_b32 s75, s28
	s_movk_i32 s43, 0x6000
	s_waitcnt vmcnt(0)
	v_lshlrev_b32_e32 v26, 16, v26
	v_cndmask_b32_e64 v49, -v26, v26, vcc
	v_sub_u32_e32 v26, 0x2400, v18
	v_cmp_eq_u32_e32 vcc, s67, v18
	s_mov_b32 s67, s24
	s_nop 0
	v_cndmask_b32_e64 v26, v26, 0, vcc
	v_ashrrev_i32_e32 v27, 31, v26
	v_lshl_add_u64 v[26:27], v[26:27], 1, s[2:3]
	global_load_ushort v44, v[26:27], off
	s_nop 0
	global_load_ushort v46, v[46:47], off
	s_nop 0
	global_load_ushort v47, v[50:51], off
	global_load_ushort v48, v[52:53], off
	s_nop 0
	global_load_ushort v50, v[54:55], off
	v_sub_u32_e32 v26, 0x1a00, v18
	v_cndmask_b32_e64 v26, v26, 0, s[10:11]
	v_ashrrev_i32_e32 v27, 31, v26
	v_lshl_add_u64 v[26:27], v[26:27], 1, s[2:3]
	global_load_ushort v26, v[26:27], off
	s_nop 0
	global_load_ushort v53, v[28:29], off offset:1024
	global_load_ushort v51, v[28:29], off offset:2048
	s_waitcnt vmcnt(7)
	v_lshlrev_b32_e32 v27, 16, v44
	v_cndmask_b32_e64 v61, -v27, v27, vcc
	s_waitcnt vmcnt(6)
	v_lshlrev_b32_e32 v27, 16, v46
	v_cndmask_b32_e64 v63, -v27, v27, s[8:9]
	s_waitcnt vmcnt(5)
	v_lshlrev_b32_e32 v27, 16, v47
	v_cndmask_b32_e64 v90, -v27, v27, s[6:7]
	s_waitcnt vmcnt(4)
	v_lshlrev_b32_e32 v27, 16, v48
	v_cndmask_b32_e64 v59, -v27, v27, s[4:5]
	s_waitcnt vmcnt(3)
	v_lshlrev_b32_e32 v27, 16, v50
	v_cndmask_b32_e64 v57, -v27, v27, s[0:1]
	v_sub_u32_e32 v44, 0x1800, v18
	v_cmp_eq_u32_e64 s[8:9], s56, v18
	s_movk_i32 s0, 0xd600
	s_waitcnt vmcnt(2)
	v_lshlrev_b32_e32 v26, 16, v26
	v_cndmask_b32_e64 v46, v44, 0, s[8:9]
	v_sub_u32_e32 v44, 0x1600, v18
	v_cmp_eq_u32_e64 s[6:7], s0, v18
	s_movk_i32 s0, 0xd400
	v_cndmask_b32_e64 v55, -v26, v26, s[10:11]
	v_add_co_u32_e32 v26, vcc, s12, v16
	v_cndmask_b32_e64 v64, v44, 0, s[6:7]
	v_sub_u32_e32 v44, 0x1400, v18
	v_cmp_eq_u32_e64 s[4:5], s0, v18
	s_movk_i32 s0, 0xd200
	v_addc_co_u32_e32 v27, vcc, 0, v17, vcc
	v_cndmask_b32_e64 v66, v44, 0, s[4:5]
	v_sub_u32_e32 v44, 0x1200, v18
	v_cmp_eq_u32_e64 s[0:1], s0, v18
	s_movk_i32 s10, 0xd000
	v_cmp_eq_u32_e32 vcc, s10, v18
	v_cndmask_b32_e64 v68, v44, 0, s[0:1]
	v_sub_u32_e32 v44, 0x1000, v18
	v_ashrrev_i32_e32 v47, 31, v46
	v_cndmask_b32_e64 v70, v44, 0, vcc
	v_lshl_add_u64 v[46:47], v[46:47], 1, s[2:3]
	v_ashrrev_i32_e32 v65, 31, v64
	v_ashrrev_i32_e32 v67, 31, v66
	v_ashrrev_i32_e32 v69, 31, v68
	v_ashrrev_i32_e32 v71, 31, v70
	v_lshl_add_u64 v[64:65], v[64:65], 1, s[2:3]
	v_lshl_add_u64 v[66:67], v[66:67], 1, s[2:3]
	v_lshl_add_u64 v[68:69], v[68:69], 1, s[2:3]
	v_lshl_add_u64 v[70:71], v[70:71], 1, s[2:3]
	global_load_ushort v44, v[46:47], off
	global_load_ushort v48, v[64:65], off
	global_load_ushort v50, v[66:67], off
	global_load_ushort v52, v[68:69], off
	global_load_ushort v54, v[70:71], off
	v_sub_u32_e32 v46, 0xe00, v18
	v_cmp_eq_u32_e64 s[12:13], s84, v18
	s_movk_i32 s10, 0xcc00
	v_cmp_eq_u32_e64 s[10:11], s10, v18
	v_cndmask_b32_e64 v46, v46, 0, s[12:13]
	v_ashrrev_i32_e32 v47, 31, v46
	v_lshl_add_u64 v[46:47], v[46:47], 1, s[2:3]
	global_load_ushort v56, v[46:47], off
	v_sub_u32_e32 v46, 0xc00, v18
	v_cndmask_b32_e64 v46, v46, 0, s[10:11]
	v_ashrrev_i32_e32 v47, 31, v46
	v_lshl_add_u64 v[46:47], v[46:47], 1, s[2:3]
	global_load_ushort v46, v[46:47], off
	s_nop 0
	global_load_ushort v91, v[28:29], off offset:3072
	s_mov_b32 s84, 0x3f3504f3
	s_mov_b32 s85, 0xbf3504f3
	s_mov_b32 s54, s85
	s_mov_b32 s55, s84
	s_mov_b32 s56, s19
	s_mov_b32 s38, s85
	s_waitcnt vmcnt(7)
	v_lshlrev_b32_e32 v28, 16, v44
	v_cndmask_b32_e64 v97, -v28, v28, s[8:9]
	s_waitcnt vmcnt(6)
	v_lshlrev_b32_e32 v28, 16, v48
	v_cndmask_b32_e64 v96, -v28, v28, s[6:7]
	s_waitcnt vmcnt(5)
	v_lshlrev_b32_e32 v28, 16, v50
	v_cndmask_b32_e64 v94, -v28, v28, s[4:5]
	s_waitcnt vmcnt(4)
	v_lshlrev_b32_e32 v28, 16, v52
	v_cndmask_b32_e64 v93, -v28, v28, s[0:1]
	s_waitcnt vmcnt(3)
	v_lshlrev_b32_e32 v28, 16, v54
	v_cndmask_b32_e64 v92, -v28, v28, vcc
	s_movk_i32 s0, 0xca00
	v_cmp_eq_u32_e64 s[0:1], s0, v18
	s_waitcnt vmcnt(2)
	v_lshlrev_b32_e32 v28, 16, v56
	v_cndmask_b32_e64 v95, -v28, v28, s[12:13]
	v_sub_u32_e32 v28, 0xa00, v18
	v_cndmask_b32_e64 v28, v28, 0, s[0:1]
	v_ashrrev_i32_e32 v29, 31, v28
	v_lshl_add_u64 v[28:29], v[28:29], 1, s[2:3]
	global_load_ushort v44, v[28:29], off
	s_waitcnt vmcnt(2)
	v_lshlrev_b32_e32 v28, 16, v46
	v_cndmask_b32_e64 v106, -v28, v28, s[10:11]
	v_add_co_u32_e32 v28, vcc, s16, v16
	s_movk_i32 s4, 0xc400
	s_nop 0
	v_addc_co_u32_e32 v29, vcc, 0, v17, vcc
	v_sub_u32_e32 v46, 0x400, v18
	v_cmp_eq_u32_e32 vcc, s4, v18
	s_movk_i32 s4, 0xc800
	v_sub_u32_e32 v48, 0x800, v18
	v_cndmask_b32_e64 v46, v46, 0, vcc
	v_cmp_eq_u32_e64 s[4:5], s4, v18
	v_ashrrev_i32_e32 v47, 31, v46
	v_lshl_add_u64 v[46:47], v[46:47], 1, s[2:3]
	v_cndmask_b32_e64 v64, v48, 0, s[4:5]
	v_ashrrev_i32_e32 v65, 31, v64
	v_lshl_add_u64 v[64:65], v[64:65], 1, s[2:3]
	global_load_ushort v48, v[46:47], off
	s_nop 0
	global_load_ushort v46, v[64:65], off
	global_load_ushort v110, v[28:29], off
	global_load_ushort v112, v[28:29], off offset:1024
	global_load_ushort v114, v[28:29], off offset:2048
	global_load_ushort v116, v[28:29], off offset:3072
	s_mov_b32 s6, 0x3f7b14be
	s_mov_b32 s7, 0xbe47c5c2
	s_mov_b32 s16, 0x3f6c835e
	s_mov_b32 s17, 0xbec3ef15
	s_mov_b32 s50, s17
	s_mov_b32 s51, s16
	v_add_f32_e32 v50, v15, v13
	s_mov_b32 s8, 0x3e47c5c2
	s_mov_b32 s9, 0xbf7b14be
	s_mov_b32 s30, s9
	s_mov_b32 s31, s8
	s_mov_b32 s10, s93
	s_mov_b32 s11, s81
	s_mov_b32 s12, s17
	s_mov_b32 s13, s19
	s_waitcnt vmcnt(6)
	v_lshlrev_b32_e32 v28, 16, v44
	v_cndmask_b32_e64 v108, -v28, v28, s[0:1]
	s_movk_i32 s0, 0xc600
	v_sub_u32_e32 v28, 0x600, v18
	v_sub_u32_e32 v44, 0x200, v18
	s_waitcnt vmcnt(4)
	v_lshlrev_b32_e32 v29, 16, v46
	v_cndmask_b32_e64 v111, -v29, v29, s[4:5]
	v_cmp_eq_u32_e64 s[4:5], s0, v18
	s_movk_i32 s0, 0xc200
	v_cmp_eq_u32_e64 s[0:1], s0, v18
	v_cndmask_b32_e64 v28, v28, 0, s[4:5]
	v_ashrrev_i32_e32 v29, 31, v28
	v_cndmask_b32_e64 v46, v44, 0, s[0:1]
	v_lshl_add_u64 v[28:29], v[28:29], 1, s[2:3]
	v_ashrrev_i32_e32 v47, 31, v46
	v_lshl_add_u64 v[46:47], v[46:47], 1, s[2:3]
	global_load_ushort v18, v[16:17], off
	s_nop 0
	global_load_ushort v28, v[28:29], off
	s_nop 0
	global_load_ushort v29, v[16:17], off offset:1024
	s_nop 0
	global_load_ushort v17, v[16:17], off offset:2048
	s_nop 0
	global_load_ushort v44, v[46:47], off
	global_load_ushort v58, v[22:23], off offset:1024
	global_load_ushort v62, v[22:23], off offset:2048
	global_load_ushort v68, v[22:23], off offset:3072
	global_load_ushort v69, v[24:25], off offset:-4096
	global_load_ushort v98, v[24:25], off
	global_load_ushort v52, v[22:23], off offset:-4096
	global_load_ushort v54, v[20:21], off offset:1024
	s_nop 0
	global_load_ushort v21, v[20:21], off offset:2048
	s_nop 0
	global_load_ushort v56, v[22:23], off
	s_mov_b32 s2, 0x3f7ec46d
	s_mov_b32 s3, 0xbdc8bd36
	v_lshlrev_b32_e32 v22, 16, v48
	s_mov_b32 s76, s3
	s_mov_b32 s77, s2
	v_cndmask_b32_e64 v115, -v22, v22, vcc
	v_pk_mul_f32 v[22:23], v[14:15], s[76:77] op_sel_hi:[0,1] neg_lo:[1,0]
	s_mov_b64 vcc, s[64:65]
	s_mov_b32 s64, s7
	s_mov_b32 s65, s6
	s_waitcnt vmcnt(13)
	v_lshlrev_b32_e32 v16, 16, v18
	s_waitcnt vmcnt(12)
	v_lshlrev_b32_e32 v18, 16, v28
	s_waitcnt vmcnt(11)
	v_lshlrev_b32_e32 v20, 16, v29
	s_waitcnt vmcnt(10)
	v_lshlrev_b32_e32 v17, 16, v17
	v_add_f32_e32 v20, v31, v20
	v_pk_fma_f32 v[28:29], v[10:11], s[2:3], v[22:23] op_sel_hi:[0,1,1]
	v_add_f32_e32 v22, v30, v17
	v_pk_mul_f32 v[30:31], v[14:15], s[64:65] op_sel_hi:[0,1] neg_lo:[1,0]
	v_pk_fma_f32 v[46:47], v[10:11], s[6:7], v[30:31] op_sel_hi:[0,1,1]
	v_pk_mul_f32 v[30:31], v[14:15], s[78:79] op_sel_hi:[0,1] neg_lo:[1,0]
	v_pk_fma_f32 v[88:89], v[10:11], s[80:81], v[30:31] op_sel_hi:[0,1,1]
	s_waitcnt vmcnt(3)
	v_lshlrev_b32_e32 v13, 16, v52
	v_pk_mul_f32 v[30:31], v[14:15], s[50:51] op_sel_hi:[0,1] neg_lo:[1,0]
	v_add_f32_e32 v16, v19, v16
	v_cndmask_b32_e64 v113, -v18, v18, s[4:5]
	v_pk_mul_f32 v[18:19], v[14:15], s[40:41] op_sel_hi:[0,1] neg_lo:[1,0]
	v_add_f32_e32 v52, v33, v13
	v_pk_fma_f32 v[84:85], v[10:11], s[16:17], v[30:31] op_sel_hi:[0,1,1]
	s_waitcnt vmcnt(2)
	v_lshlrev_b32_e32 v13, 16, v54
	v_pk_mul_f32 v[30:31], v[14:15], s[48:49] op_sel_hi:[0,1] neg_lo:[1,0]
	s_waitcnt vmcnt(1)
	v_lshlrev_b32_e32 v15, 16, v21
	v_lshlrev_b32_e32 v17, 16, v44
	v_add_f32_e32 v44, v34, v13
	global_load_ushort v13, v[24:25], off offset:1024
	global_load_ushort v33, v[26:27], off
	v_add_f32_e32 v48, v35, v15
	global_load_ushort v15, v[24:25], off offset:2048
	v_lshlrev_b32_e32 v21, 16, v32
	s_waitcnt vmcnt(3)
	v_lshlrev_b32_e32 v23, 16, v56
	v_add_f32_e32 v54, v36, v21
	global_load_ushort v21, v[24:25], off offset:3072
	v_add_f32_e32 v56, v37, v23
	v_lshlrev_b32_e32 v23, 16, v58
	v_add_f32_e32 v60, v43, v23
	global_load_ushort v23, v[26:27], off offset:-4096
	v_pk_fma_f32 v[64:65], v[10:11], s[20:21], v[30:31] op_sel_hi:[0,1,1]
	s_mov_b32 s4, 0x3dc8bd36
	s_mov_b32 s5, 0xbf7ec46d
	s_mov_b32 s34, s5
	s_mov_b32 s35, s4
	s_mov_b32 s2, s5
	v_cndmask_b32_e64 v17, -v17, v17, s[0:1]
	s_mov_b32 s0, s3
	s_mov_b32 s1, s5
	s_mov_b32 s6, s9
	s_mov_b32 s16, s19
	s_mov_b32 s20, s89
	v_pk_fma_f32 v[18:19], v[10:11], s[44:45], v[18:19] op_sel_hi:[0,1,1]
	s_waitcnt vmcnt(4)
	v_lshlrev_b32_e32 v13, 16, v13
	s_waitcnt vmcnt(2)
	v_pk_mul_f32 v[24:25], v[14:15], s[54:55] op_sel_hi:[0,1] neg_lo:[1,0]
	v_pk_fma_f32 v[78:79], v[10:11], s[84:85], v[24:25] op_sel_hi:[0,1,1]
	v_pk_mul_f32 v[24:25], v[14:15], s[60:61] op_sel_hi:[0,1] neg_lo:[1,0]
	v_pk_fma_f32 v[86:87], v[10:11], s[86:87], v[24:25] op_sel_hi:[0,1,1]
	v_lshlrev_b32_e32 v24, 16, v62
	v_add_f32_e32 v62, v41, v24
	v_pk_mul_f32 v[24:25], v[14:15], s[66:67] op_sel_hi:[0,1] neg_lo:[1,0]
	v_pk_fma_f32 v[82:83], v[10:11], s[24:25], v[24:25] op_sel_hi:[0,1,1]
	v_lshlrev_b32_e32 v24, 16, v68
	v_add_f32_e32 v58, v42, v24
	v_pk_mul_f32 v[24:25], v[14:15], s[68:69] op_sel_hi:[0,1] neg_lo:[1,0]
	v_pk_fma_f32 v[80:81], v[10:11], s[88:89], v[24:25] op_sel_hi:[0,1,1]
	v_lshlrev_b32_e32 v24, 16, v69
	v_add_f32_e32 v42, v45, v24
	v_pk_mul_f32 v[24:25], v[14:15], s[56:57] op_sel_hi:[0,1] neg_lo:[1,0]
	v_pk_fma_f32 v[74:75], v[10:11], s[18:19], v[24:25] op_sel_hi:[0,1,1]
	v_lshlrev_b32_e32 v24, 16, v38
	v_add_f32_e32 v38, v49, v24
	v_pk_mul_f32 v[24:25], v[14:15], s[62:63] op_sel_hi:[0,1] neg_lo:[1,0]
	v_pk_fma_f32 v[72:73], v[10:11], s[92:93], v[24:25] op_sel_hi:[0,1,1]
	v_lshlrev_b32_e32 v25, 16, v39
	v_add_f32_e32 v32, v63, v25
	global_load_ushort v25, v[26:27], off offset:1024
	global_load_ushort v39, v[26:27], off offset:2048
	v_lshlrev_b32_e32 v24, 16, v40
	global_load_ushort v40, v[26:27], off offset:3072
	v_pk_mul_f32 v[30:31], v[14:15], s[58:59] op_sel_hi:[0,1] neg_lo:[1,0]
	v_pk_fma_f32 v[66:67], v[10:11], s[82:83], v[30:31] op_sel_hi:[0,1,1]
	v_pk_mul_f32 v[30:31], v[14:15], s[74:75] op_sel_hi:[0,1] neg_lo:[1,0]
	v_pk_fma_f32 v[76:77], v[10:11], s[28:29], v[30:31] op_sel_hi:[0,1,1]
	v_pk_mul_f32 v[30:31], v[14:15], s[30:31] op_sel_hi:[0,1] neg_lo:[1,0]
	v_pk_fma_f32 v[68:69], v[10:11], s[8:9], v[30:31] op_sel_hi:[0,1,1]
	v_pk_mul_f32 v[30:31], v[14:15], s[34:35] op_sel_hi:[0,1] neg_lo:[1,0]
	v_pk_fma_f32 v[70:71], v[10:11], s[4:5], v[30:31] op_sel_hi:[0,1,1]
	v_lshlrev_b32_e32 v30, 16, v98
	v_pk_mul_f32 v[34:35], v[14:15], s[36:37] op_sel_hi:[0,1] neg_lo:[1,0]
	v_add_f32_e32 v30, v90, v30
	v_pk_fma_f32 v[34:35], v[10:11], s[96:97], v[34:35] op_sel_hi:[0,1,1]
	v_pk_mul_f32 v[36:37], v[34:35], v[30:31] op_sel_hi:[1,0]
	v_pk_mul_f32 v[30:31], v[14:15], s[2:3] op_sel_hi:[0,1] neg_lo:[1,0]
	v_add_f32_e32 v26, v59, v13
	v_pk_fma_f32 v[30:31], v[10:11], s[0:1], v[30:31] op_sel_hi:[0,1,1]
	v_lshlrev_b32_e32 v13, 16, v15
	s_mov_b32 s4, s7
	s_mov_b32 s5, s9
	v_pk_mul_f32 v[34:35], v[14:15], s[6:7] op_sel_hi:[0,1] neg_lo:[1,0]
	v_pk_mul_f32 v[26:27], v[30:31], v[26:27] op_sel_hi:[1,0]
	v_add_f32_e32 v30, v57, v13
	v_pk_fma_f32 v[34:35], v[10:11], s[4:5], v[34:35] op_sel_hi:[0,1,1]
	v_pk_mul_f32 v[98:99], v[34:35], v[30:31] op_sel_hi:[1,0]
	s_waitcnt vmcnt(4)
	v_lshlrev_b32_e32 v13, 16, v21
	s_mov_b32 s8, s81
	s_mov_b32 s9, s93
	v_pk_mul_f32 v[34:35], v[14:15], s[10:11] op_sel_hi:[0,1] neg_lo:[1,0]
	v_add_f32_e32 v30, v55, v13
	v_pk_fma_f32 v[34:35], v[10:11], s[8:9], v[34:35] op_sel_hi:[0,1,1]
	v_pk_mul_f32 v[100:101], v[34:35], v[30:31] op_sel_hi:[1,0]
	s_waitcnt vmcnt(3)
	v_lshlrev_b32_e32 v13, 16, v23
	v_pk_mul_f32 v[34:35], v[14:15], s[16:17] op_sel_hi:[0,1] neg_lo:[1,0]
	v_add_f32_e32 v30, v97, v13
	v_pk_fma_f32 v[34:35], v[10:11], s[12:13], v[34:35] op_sel_hi:[0,1,1]
	v_pk_mul_f32 v[102:103], v[34:35], v[30:31] op_sel_hi:[1,0]
	v_lshlrev_b32_e32 v13, 16, v53
	s_mov_b32 s18, s21
	s_mov_b32 s19, s89
	v_pk_mul_f32 v[34:35], v[14:15], s[20:21] op_sel_hi:[0,1] neg_lo:[1,0]
	v_add_f32_e32 v30, v96, v13
	v_pk_fma_f32 v[34:35], v[10:11], s[18:19], v[34:35] op_sel_hi:[0,1,1]
	s_mov_b32 s24, s25
	s_mov_b32 s25, s83
	v_pk_mul_f32 v[96:97], v[34:35], v[30:31] op_sel_hi:[1,0]
	v_lshlrev_b32_e32 v13, 16, v51
	v_pk_mul_f32 v[34:35], v[14:15], s[24:25] op_sel_hi:[0,1] neg_lo:[1,0]
	v_add_f32_e32 v30, v94, v13
	v_pk_fma_f32 v[34:35], v[10:11], s[22:23], v[34:35] op_sel_hi:[0,1,1]
	s_mov_b32 s28, s87
	v_pk_mul_f32 v[104:105], v[34:35], v[30:31] op_sel_hi:[1,0]
	v_lshlrev_b32_e32 v13, 16, v91
	v_pk_mul_f32 v[34:35], v[14:15], s[28:29] op_sel_hi:[0,1] neg_lo:[1,0]
	v_add_f32_e32 v30, v93, v13
	v_pk_fma_f32 v[34:35], v[10:11], s[26:27], v[34:35] op_sel_hi:[0,1,1]
	v_pk_mul_f32 v[90:91], v[34:35], v[30:31] op_sel_hi:[1,0]
	v_lshlrev_b32_e32 v13, 16, v33
	v_pk_mul_f32 v[34:35], v[14:15], s[84:85] op_sel_hi:[0,0] neg_lo:[1,0]
	v_add_f32_e32 v30, v92, v13
	v_pk_fma_f32 v[34:35], v[10:11], s[38:39], v[34:35] op_sel_hi:[0,0,1] neg_lo:[0,0,1] neg_hi:[0,0,1]
	v_pk_mul_f32 v[92:93], v[34:35], v[30:31] op_sel_hi:[1,0]
	v_pk_mul_f32 v[34:35], v[14:15], s[26:27] op_sel_hi:[0,1] neg_lo:[1,0]
	v_pk_fma_f32 v[34:35], v[10:11], s[28:29], v[34:35] op_sel_hi:[0,1,1]
	v_add_f32_e32 v24, v61, v24
	s_waitcnt vmcnt(2)
	v_lshlrev_b32_e32 v13, 16, v25
	v_add_f32_e32 v30, v95, v13
	v_pk_mul_f32 v[94:95], v[34:35], v[30:31] op_sel_hi:[1,0]
	s_waitcnt vmcnt(1)
	v_lshlrev_b32_e32 v13, 16, v39
	v_pk_mul_f32 v[34:35], v[14:15], s[22:23] op_sel_hi:[0,1] neg_lo:[1,0]
	v_add_f32_e32 v30, v106, v13
	v_pk_fma_f32 v[34:35], v[10:11], s[24:25], v[34:35] op_sel_hi:[0,1,1]
	v_pk_mul_f32 v[106:107], v[34:35], v[30:31] op_sel_hi:[1,0]
	s_waitcnt vmcnt(0)
	v_lshlrev_b32_e32 v13, 16, v40
	v_pk_mul_f32 v[34:35], v[14:15], s[18:19] op_sel_hi:[0,1] neg_lo:[1,0]
	v_add_f32_e32 v30, v108, v13
	v_pk_fma_f32 v[34:35], v[10:11], s[20:21], v[34:35] op_sel_hi:[0,1,1]
	v_pk_mul_f32 v[108:109], v[34:35], v[30:31] op_sel_hi:[1,0]
	v_lshlrev_b32_e32 v13, 16, v110
	v_pk_mul_f32 v[34:35], v[14:15], s[12:13] op_sel_hi:[0,1] neg_lo:[1,0]
	v_add_f32_e32 v30, v111, v13
	v_pk_fma_f32 v[34:35], v[10:11], s[16:17], v[34:35] op_sel_hi:[0,1,1]
	v_pk_mul_f32 v[110:111], v[34:35], v[30:31] op_sel_hi:[1,0]
	v_lshlrev_b32_e32 v13, 16, v112
	v_pk_mul_f32 v[34:35], v[14:15], s[8:9] op_sel_hi:[0,1] neg_lo:[1,0]
	v_add_f32_e32 v30, v113, v13
	v_pk_fma_f32 v[34:35], v[10:11], s[10:11], v[34:35] op_sel_hi:[0,1,1]
	v_pk_mul_f32 v[112:113], v[34:35], v[30:31] op_sel_hi:[1,0]
	v_lshlrev_b32_e32 v13, 16, v114
	v_pk_mul_f32 v[34:35], v[14:15], s[4:5] op_sel_hi:[0,1] neg_lo:[1,0]
	v_add_f32_e32 v30, v115, v13
	v_pk_fma_f32 v[34:35], v[10:11], s[6:7], v[34:35] op_sel_hi:[0,1,1]
	v_lshlrev_b32_e32 v13, 16, v116
	v_pk_mul_f32 v[14:15], v[14:15], s[0:1] op_sel_hi:[0,1] neg_lo:[1,0]
	v_pk_mul_f32 v[114:115], v[34:35], v[30:31] op_sel_hi:[1,0]
	v_add_f32_e32 v30, v17, v13
	v_pk_fma_f32 v[14:15], v[10:11], s[2:3], v[14:15] op_sel_hi:[0,1,1]
	v_pk_mul_f32 v[116:117], v[14:15], v[30:31] op_sel_hi:[1,0]
	v_mov_b32_e32 v13, v173
	v_mov_b32_e32 v10, v1
	v_mov_b32_e32 v30, v165
	v_mov_b32_e32 v10, v167
	v_mov_b32_e32 v34, v169
	v_mov_b32_e32 v17, v171
	s_nop 0
	v_pk_fma_f32 v[126:127], v[18:19], v[16:17], v[36:37] op_sel_hi:[1,0,1]
	v_pk_fma_f32 v[36:37], v[18:19], v[16:17], v[36:37] op_sel_hi:[1,0,1] neg_lo:[0,0,1] neg_hi:[0,0,1]
	v_pk_fma_f32 v[18:19], v[28:29], v[20:21], v[26:27] op_sel_hi:[1,0,1] neg_lo:[0,0,1] neg_hi:[0,0,1]
	v_pk_fma_f32 v[16:17], v[28:29], v[20:21], v[26:27] op_sel_hi:[1,0,1]
	v_pk_mul_f32 v[20:21], v[18:19], v[124:125] op_sel:[1,0] op_sel_hi:[0,0] neg_lo:[1,1] neg_hi:[0,1]
	v_pk_fma_f32 v[40:41], v[18:19], v[118:119], v[20:21] op_sel_hi:[1,0,1]
	v_pk_fma_f32 v[20:21], v[46:47], v[22:23], v[98:99] op_sel_hi:[1,0,1] neg_lo:[0,0,1] neg_hi:[0,0,1]
	v_pk_fma_f32 v[18:19], v[46:47], v[22:23], v[98:99] op_sel_hi:[1,0,1]
	v_pk_mul_f32 v[22:23], v[20:21], v[34:35] op_sel:[1,0] op_sel_hi:[0,0] neg_lo:[1,1] neg_hi:[0,1]
	v_pk_fma_f32 v[46:47], v[20:21], v[30:31], v[22:23] op_sel_hi:[1,0,1]
	v_pk_fma_f32 v[22:23], v[88:89], v[50:51], v[100:101] op_sel_hi:[1,0,1] neg_lo:[0,0,1] neg_hi:[0,0,1]
	v_pk_fma_f32 v[20:21], v[88:89], v[50:51], v[100:101] op_sel_hi:[1,0,1]
	v_pk_mul_f32 v[26:27], v[22:23], v[122:123] op_sel:[1,0] op_sel_hi:[0,0] neg_lo:[1,1] neg_hi:[0,1]
	v_pk_fma_f32 v[50:51], v[22:23], v[120:121], v[26:27] op_sel_hi:[1,0,1]
	v_pk_fma_f32 v[26:27], v[84:85], v[52:53], v[102:103] op_sel_hi:[1,0,1] neg_lo:[0,0,1] neg_hi:[0,0,1]
	v_pk_fma_f32 v[22:23], v[84:85], v[52:53], v[102:103] op_sel_hi:[1,0,1]
	v_pk_mul_f32 v[28:29], v[26:27], v[10:11] op_sel:[1,0] op_sel_hi:[0,0] neg_lo:[1,1] neg_hi:[0,1]
	v_pk_fma_f32 v[52:53], v[26:27], v[10:11], v[28:29] op_sel_hi:[1,0,1]
	v_pk_fma_f32 v[28:29], v[64:65], v[44:45], v[96:97] op_sel_hi:[1,0,1] neg_lo:[0,0,1] neg_hi:[0,0,1]
	v_pk_fma_f32 v[26:27], v[64:65], v[44:45], v[96:97] op_sel_hi:[1,0,1]
	v_pk_mul_f32 v[44:45], v[28:29], v[122:123] op_sel_hi:[1,0]
	v_pk_fma_f32 v[64:65], v[28:29], v[120:121], v[44:45] op_sel:[1,0,0] op_sel_hi:[0,0,1] neg_lo:[1,1,0] neg_hi:[0,1,0]
	v_pk_fma_f32 v[44:45], v[66:67], v[48:49], v[104:105] op_sel_hi:[1,0,1] neg_lo:[0,0,1] neg_hi:[0,0,1]
	v_pk_fma_f32 v[28:29], v[66:67], v[48:49], v[104:105] op_sel_hi:[1,0,1]
	v_pk_mul_f32 v[48:49], v[44:45], v[34:35] op_sel_hi:[1,0]
	v_pk_fma_f32 v[66:67], v[44:45], v[30:31], v[48:49] op_sel:[1,0,0] op_sel_hi:[0,0,1] neg_lo:[1,1,0] neg_hi:[0,1,0]
	v_pk_fma_f32 v[48:49], v[76:77], v[54:55], v[90:91] op_sel_hi:[1,0,1] neg_lo:[0,0,1] neg_hi:[0,0,1]
	v_pk_fma_f32 v[44:45], v[76:77], v[54:55], v[90:91] op_sel_hi:[1,0,1]
	v_pk_mul_f32 v[54:55], v[48:49], v[124:125] op_sel_hi:[1,0]
	v_xor_b32_e32 v76, 0x80000000, v49
	v_mov_b32_e32 v77, v48
	v_pk_fma_f32 v[48:49], v[78:79], v[56:57], v[92:93] op_sel_hi:[1,0,1]
	v_pk_fma_f32 v[56:57], v[78:79], v[56:57], v[92:93] op_sel_hi:[1,0,1] neg_lo:[0,0,1] neg_hi:[0,0,1]
	v_pk_fma_f32 v[54:55], v[76:77], v[118:119], v[54:55] op_sel_hi:[1,0,1] neg_lo:[0,1,0] neg_hi:[0,1,0]
	v_xor_b32_e32 v77, 0x80000000, v56
	v_mov_b32_e32 v76, v57
	v_pk_fma_f32 v[56:57], v[86:87], v[60:61], v[94:95] op_sel_hi:[1,0,1]
	v_pk_fma_f32 v[60:61], v[86:87], v[60:61], v[94:95] op_sel_hi:[1,0,1] neg_lo:[0,0,1] neg_hi:[0,0,1]
	v_pk_mul_f32 v[78:79], v[60:61], v[124:125] op_sel_hi:[1,0] neg_lo:[0,1] neg_hi:[0,1]
	v_pk_fma_f32 v[60:61], v[60:61], v[118:119], v[78:79] op_sel:[1,0,0] op_sel_hi:[0,0,1] neg_lo:[1,1,0] neg_hi:[0,1,0]
	v_pk_fma_f32 v[78:79], v[82:83], v[62:63], v[106:107] op_sel_hi:[1,0,1]
	v_pk_fma_f32 v[62:63], v[82:83], v[62:63], v[106:107] op_sel_hi:[1,0,1] neg_lo:[0,0,1] neg_hi:[0,0,1]
	v_pk_mul_f32 v[82:83], v[62:63], v[34:35] op_sel_hi:[1,0] neg_lo:[0,1] neg_hi:[0,1]
	v_pk_fma_f32 v[62:63], v[62:63], v[30:31], v[82:83] op_sel:[1,0,0] op_sel_hi:[0,0,1] neg_lo:[1,1,0] neg_hi:[0,1,0]
	v_pk_fma_f32 v[82:83], v[80:81], v[58:59], v[108:109] op_sel_hi:[1,0,1]
	v_pk_fma_f32 v[58:59], v[80:81], v[58:59], v[108:109] op_sel_hi:[1,0,1] neg_lo:[0,0,1] neg_hi:[0,0,1]
	v_pk_mul_f32 v[80:81], v[58:59], v[122:123] op_sel_hi:[1,0] neg_lo:[0,1] neg_hi:[0,1]
	v_pk_fma_f32 v[58:59], v[58:59], v[120:121], v[80:81] op_sel:[1,0,0] op_sel_hi:[0,0,1] neg_lo:[1,1,0] neg_hi:[0,1,0]
	v_pk_add_f32 v[84:85], v[16:17], v[56:57]
	v_pk_add_f32 v[16:17], v[16:17], v[56:57] neg_lo:[0,1] neg_hi:[0,1]
	v_pk_fma_f32 v[80:81], v[74:75], v[42:43], v[110:111] op_sel_hi:[1,0,1]
	v_pk_mul_f32 v[56:57], v[16:17], v[34:35] op_sel:[1,0] op_sel_hi:[0,0] neg_lo:[1,1] neg_hi:[0,1]
	v_pk_fma_f32 v[42:43], v[74:75], v[42:43], v[110:111] op_sel_hi:[1,0,1] neg_lo:[0,0,1] neg_hi:[0,0,1]
	v_pk_fma_f32 v[56:57], v[16:17], v[30:31], v[56:57] op_sel_hi:[1,0,1]
	v_pk_add_f32 v[16:17], v[18:19], v[78:79]
	v_pk_add_f32 v[18:19], v[18:19], v[78:79] neg_lo:[0,1] neg_hi:[0,1]
	v_pk_mul_f32 v[74:75], v[42:43], v[10:11] op_sel:[1,0] op_sel_hi:[0,0] neg_lo:[1,1] neg_hi:[0,1]
	v_pk_mul_f32 v[78:79], v[18:19], v[10:11] op_sel:[1,0] op_sel_hi:[0,0] neg_lo:[1,1] neg_hi:[0,1]
	v_pk_fma_f32 v[74:75], v[42:43], v[10:11], v[74:75] op_sel_hi:[1,0,1] neg_lo:[0,1,0] neg_hi:[0,1,0]
	v_pk_fma_f32 v[42:43], v[72:73], v[38:39], v[112:113] op_sel_hi:[1,0,1]
	v_pk_fma_f32 v[38:39], v[72:73], v[38:39], v[112:113] op_sel_hi:[1,0,1] neg_lo:[0,0,1] neg_hi:[0,0,1]
	v_pk_fma_f32 v[18:19], v[18:19], v[10:11], v[78:79] op_sel_hi:[1,0,1]
	v_pk_add_f32 v[78:79], v[20:21], v[82:83]
	v_pk_add_f32 v[20:21], v[20:21], v[82:83] neg_lo:[0,1] neg_hi:[0,1]
	v_pk_mul_f32 v[82:83], v[20:21], v[34:35] op_sel_hi:[1,0]
	v_xor_b32_e32 v86, 0x80000000, v21
	v_mov_b32_e32 v87, v20
	v_pk_add_f32 v[20:21], v[22:23], v[80:81]
	v_pk_add_f32 v[22:23], v[22:23], v[80:81] neg_lo:[0,1] neg_hi:[0,1]
	v_pk_mul_f32 v[72:73], v[38:39], v[122:123] op_sel:[1,0] op_sel_hi:[0,0] neg_lo:[1,1] neg_hi:[0,1]
	v_xor_b32_e32 v81, 0x80000000, v22
	v_mov_b32_e32 v80, v23
	v_pk_add_f32 v[22:23], v[26:27], v[42:43]
	v_pk_add_f32 v[26:27], v[26:27], v[42:43] neg_lo:[0,1] neg_hi:[0,1]
	v_pk_fma_f32 v[72:73], v[38:39], v[120:121], v[72:73] op_sel_hi:[1,0,1] neg_lo:[0,1,0] neg_hi:[0,1,0]
	v_pk_fma_f32 v[38:39], v[68:69], v[24:25], v[114:115] op_sel_hi:[1,0,1]
	v_pk_fma_f32 v[24:25], v[68:69], v[24:25], v[114:115] op_sel_hi:[1,0,1] neg_lo:[0,0,1] neg_hi:[0,0,1]
	v_pk_fma_f32 v[82:83], v[86:87], v[30:31], v[82:83] op_sel_hi:[1,0,1] neg_lo:[0,1,0] neg_hi:[0,1,0]
	v_pk_mul_f32 v[42:43], v[26:27], v[34:35] op_sel_hi:[1,0] neg_lo:[0,1] neg_hi:[0,1]
	v_pk_fma_f32 v[26:27], v[30:31], v[26:27], v[42:43] op_sel:[0,1,0] op_sel_hi:[0,0,1] neg_lo:[1,1,0] neg_hi:[1,0,0]
	v_pk_add_f32 v[42:43], v[28:29], v[38:39]
	v_pk_add_f32 v[28:29], v[28:29], v[38:39] neg_lo:[0,1] neg_hi:[0,1]
	v_pk_mul_f32 v[68:69], v[24:25], v[34:35] op_sel:[1,0] op_sel_hi:[0,0] neg_lo:[1,1] neg_hi:[0,1]
	v_pk_fma_f32 v[68:69], v[24:25], v[30:31], v[68:69] op_sel_hi:[1,0,1] neg_lo:[0,1,0] neg_hi:[0,1,0]
	v_pk_fma_f32 v[24:25], v[70:71], v[32:33], v[116:117] op_sel_hi:[1,0,1]
	v_pk_fma_f32 v[32:33], v[70:71], v[32:33], v[116:117] op_sel_hi:[1,0,1] neg_lo:[0,0,1] neg_hi:[0,0,1]
	v_pk_mul_f32 v[38:39], v[10:11], v[28:29] op_sel:[0,1] op_sel_hi:[0,0] neg_lo:[1,1] neg_hi:[1,0]
	v_pk_fma_f32 v[86:87], v[28:29], v[10:11], v[38:39] op_sel_hi:[1,0,1] neg_lo:[0,1,0] neg_hi:[0,1,0]
	v_pk_add_f32 v[28:29], v[44:45], v[24:25]
	v_pk_add_f32 v[24:25], v[44:45], v[24:25] neg_lo:[0,1] neg_hi:[0,1]
	v_pk_mul_f32 v[70:71], v[32:33], v[124:125] op_sel:[1,0] op_sel_hi:[0,0] neg_lo:[1,1] neg_hi:[0,1]
	v_pk_fma_f32 v[70:71], v[118:119], v[32:33], v[70:71] op_sel_hi:[0,1,1] neg_lo:[1,0,0] neg_hi:[1,0,0]
	v_pk_add_f32 v[32:33], v[126:127], v[48:49]
	v_pk_mul_f32 v[38:39], v[34:35], v[24:25] op_sel:[0,1] op_sel_hi:[0,0] neg_lo:[1,1] neg_hi:[1,0]
	v_pk_fma_f32 v[88:89], v[30:31], v[24:25], v[38:39] op_sel_hi:[0,1,1] neg_lo:[1,0,0] neg_hi:[1,0,0]
	v_pk_add_f32 v[24:25], v[32:33], v[20:21]
	v_pk_add_f32 v[32:33], v[32:33], v[20:21] neg_lo:[0,1] neg_hi:[0,1]
	v_pk_add_f32 v[20:21], v[84:85], v[22:23]
	v_pk_add_f32 v[22:23], v[84:85], v[22:23] neg_lo:[0,1] neg_hi:[0,1]
	v_pk_add_f32 v[48:49], v[126:127], v[48:49] neg_lo:[0,1] neg_hi:[0,1]
	v_pk_mul_f32 v[38:39], v[10:11], v[22:23] op_sel:[0,1] op_sel_hi:[0,0] neg_lo:[1,1] neg_hi:[1,0]
	v_pk_fma_f32 v[22:23], v[22:23], v[10:11], v[38:39] op_sel_hi:[1,0,1]
	v_pk_add_f32 v[38:39], v[16:17], v[42:43]
	v_pk_add_f32 v[16:17], v[16:17], v[42:43] neg_lo:[0,1] neg_hi:[0,1]
	v_xor_b32_e32 v43, 0x80000000, v16
	v_mov_b32_e32 v42, v17
	v_pk_add_f32 v[16:17], v[78:79], v[28:29]
	v_pk_add_f32 v[28:29], v[78:79], v[28:29] neg_lo:[0,1] neg_hi:[0,1]
	v_pk_mul_f32 v[44:45], v[10:11], v[28:29] op_sel:[0,1] op_sel_hi:[0,0] neg_lo:[1,1] neg_hi:[1,0]
	v_pk_fma_f32 v[78:79], v[10:11], v[28:29], v[44:45] op_sel_hi:[0,1,1] neg_lo:[1,0,0] neg_hi:[1,0,0]
	v_pk_add_f32 v[28:29], v[24:25], v[38:39]
	v_pk_add_f32 v[24:25], v[24:25], v[38:39] neg_lo:[0,1] neg_hi:[0,1]
	v_pk_add_f32 v[38:39], v[20:21], v[16:17]
	v_pk_add_f32 v[16:17], v[20:21], v[16:17] neg_lo:[0,1] neg_hi:[0,1]
	v_pk_add_f32 v[84:85], v[28:29], v[38:39]
	v_pk_add_f32 v[44:45], v[24:25], v[16:17] op_sel:[0,1] op_sel_hi:[1,0] neg_hi:[0,1]
	v_pk_add_f32 v[20:21], v[24:25], v[16:17] op_sel:[0,1] op_sel_hi:[1,0] neg_lo:[0,1]
	v_pk_add_f32 v[24:25], v[22:23], v[78:79]
	v_pk_add_f32 v[22:23], v[22:23], v[78:79] neg_lo:[0,1] neg_hi:[0,1]
	v_pk_add_f32 v[16:17], v[32:33], v[42:43]
	v_pk_add_f32 v[32:33], v[32:33], v[42:43] neg_lo:[0,1] neg_hi:[0,1]
	v_pk_add_f32 v[28:29], v[28:29], v[38:39] neg_lo:[0,1] neg_hi:[0,1]
	v_pk_add_f32 v[78:79], v[16:17], v[24:25]
	v_pk_add_f32 v[24:25], v[16:17], v[24:25] neg_lo:[0,1] neg_hi:[0,1]
	v_pk_add_f32 v[38:39], v[32:33], v[22:23] op_sel:[0,1] op_sel_hi:[1,0] neg_hi:[0,1]
	v_pk_add_f32 v[16:17], v[32:33], v[22:23] op_sel:[0,1] op_sel_hi:[1,0] neg_lo:[0,1]
	v_pk_add_f32 v[32:33], v[56:57], v[26:27]
	v_pk_add_f32 v[26:27], v[56:57], v[26:27] neg_lo:[0,1] neg_hi:[0,1]
	v_pk_add_f32 v[22:23], v[48:49], v[80:81]
	v_pk_add_f32 v[42:43], v[48:49], v[80:81] neg_lo:[0,1] neg_hi:[0,1]
	v_pk_mul_f32 v[48:49], v[10:11], v[26:27] op_sel:[0,1] op_sel_hi:[0,0] neg_lo:[1,1] neg_hi:[1,0]
	v_pk_fma_f32 v[26:27], v[10:11], v[26:27], v[48:49] op_sel_hi:[0,1,1]
	v_pk_add_f32 v[48:49], v[18:19], v[86:87]
	v_pk_add_f32 v[18:19], v[18:19], v[86:87] neg_lo:[0,1] neg_hi:[0,1]
	v_pk_add_f32 v[80:81], v[82:83], v[88:89] neg_lo:[0,1] neg_hi:[0,1]
	v_xor_b32_e32 v57, 0x80000000, v18
	v_mov_b32_e32 v56, v19
	v_pk_add_f32 v[18:19], v[82:83], v[88:89]
	v_pk_mul_f32 v[82:83], v[10:11], v[80:81] op_sel:[0,1] op_sel_hi:[0,0] neg_lo:[1,1] neg_hi:[1,0]
	v_pk_fma_f32 v[80:81], v[10:11], v[80:81], v[82:83] op_sel_hi:[0,1,1] neg_lo:[1,0,0] neg_hi:[1,0,0]
	v_pk_add_f32 v[82:83], v[22:23], v[48:49]
	v_pk_add_f32 v[22:23], v[22:23], v[48:49] neg_lo:[0,1] neg_hi:[0,1]
	v_pk_add_f32 v[48:49], v[32:33], v[18:19]
	v_pk_add_f32 v[18:19], v[32:33], v[18:19] neg_lo:[0,1] neg_hi:[0,1]
	v_pk_add_f32 v[88:89], v[82:83], v[48:49]
	v_xor_b32_e32 v87, 0x80000000, v18
	v_mov_b32_e32 v86, v19
	v_pk_add_f32 v[18:19], v[42:43], v[56:57]
	v_pk_add_f32 v[56:57], v[42:43], v[56:57] neg_lo:[0,1] neg_hi:[0,1]
	v_pk_add_f32 v[42:43], v[26:27], v[80:81]
	v_pk_add_f32 v[26:27], v[26:27], v[80:81] neg_lo:[0,1] neg_hi:[0,1]
	v_pk_add_f32 v[32:33], v[82:83], v[48:49] neg_lo:[0,1] neg_hi:[0,1]
	v_xor_b32_e32 v81, 0x80000000, v26
	v_mov_b32_e32 v80, v27
	v_pk_add_f32 v[82:83], v[18:19], v[42:43]
	v_pk_add_f32 v[26:27], v[18:19], v[42:43] neg_lo:[0,1] neg_hi:[0,1]
	v_pk_add_f32 v[42:43], v[56:57], v[80:81]
	v_pk_add_f32 v[18:19], v[56:57], v[80:81] neg_lo:[0,1] neg_hi:[0,1]
	v_pk_add_f32 v[56:57], v[36:37], v[76:77]
	v_pk_add_f32 v[76:77], v[36:37], v[76:77] neg_lo:[0,1] neg_hi:[0,1]
	v_pk_add_f32 v[36:37], v[40:41], v[60:61]
	v_pk_add_f32 v[40:41], v[40:41], v[60:61] neg_lo:[0,1] neg_hi:[0,1]
	v_pk_add_f32 v[48:49], v[22:23], v[86:87]
	v_pk_mul_f32 v[60:61], v[34:35], v[40:41] op_sel:[0,1] op_sel_hi:[0,0] neg_lo:[1,1] neg_hi:[1,0]
	v_pk_fma_f32 v[40:41], v[30:31], v[40:41], v[60:61] op_sel_hi:[0,1,1]
	v_pk_add_f32 v[60:61], v[46:47], v[62:63]
	v_pk_add_f32 v[46:47], v[46:47], v[62:63] neg_lo:[0,1] neg_hi:[0,1]
	v_pk_add_f32 v[22:23], v[22:23], v[86:87] neg_lo:[0,1] neg_hi:[0,1]
	v_pk_mul_f32 v[62:63], v[10:11], v[46:47] op_sel:[0,1] op_sel_hi:[0,0] neg_lo:[1,1] neg_hi:[1,0]
	v_pk_fma_f32 v[62:63], v[10:11], v[46:47], v[62:63] op_sel_hi:[0,1,1]
	v_pk_add_f32 v[46:47], v[50:51], v[58:59]
	v_pk_add_f32 v[50:51], v[50:51], v[58:59] neg_lo:[0,1] neg_hi:[0,1]
	v_pk_mul_f32 v[58:59], v[30:31], v[50:51] op_sel:[0,1] op_sel_hi:[0,0] neg_lo:[1,1] neg_hi:[1,0]
	v_pk_fma_f32 v[50:51], v[34:35], v[50:51], v[58:59] op_sel_hi:[0,1,1]
	v_pk_add_f32 v[58:59], v[52:53], v[74:75]
	v_pk_add_f32 v[52:53], v[52:53], v[74:75] neg_lo:[0,1] neg_hi:[0,1]
	v_xor_b32_e32 v75, 0x80000000, v52
	v_mov_b32_e32 v74, v53
	v_pk_add_f32 v[52:53], v[64:65], v[72:73]
	v_pk_add_f32 v[64:65], v[64:65], v[72:73] neg_lo:[0,1] neg_hi:[0,1]
	v_pk_mul_f32 v[72:73], v[30:31], v[64:65] op_sel:[0,1] op_sel_hi:[0,0] neg_lo:[1,1] neg_hi:[1,0]
	v_pk_fma_f32 v[64:65], v[34:35], v[64:65], v[72:73] op_sel_hi:[0,1,1] neg_lo:[1,0,0] neg_hi:[1,0,0]
	v_pk_add_f32 v[72:73], v[66:67], v[68:69]
	v_pk_add_f32 v[66:67], v[66:67], v[68:69] neg_lo:[0,1] neg_hi:[0,1]
	v_pk_mul_f32 v[68:69], v[10:11], v[66:67] op_sel:[0,1] op_sel_hi:[0,0] neg_lo:[1,1] neg_hi:[1,0]
	v_pk_fma_f32 v[66:67], v[10:11], v[66:67], v[68:69] op_sel_hi:[0,1,1] neg_lo:[1,0,0] neg_hi:[1,0,0]
	v_pk_add_f32 v[68:69], v[54:55], v[70:71]
	v_pk_add_f32 v[54:55], v[54:55], v[70:71] neg_lo:[0,1] neg_hi:[0,1]
	v_pk_mul_f32 v[34:35], v[34:35], v[54:55] op_sel:[0,1] op_sel_hi:[0,0] neg_lo:[1,1] neg_hi:[1,0]
	v_pk_fma_f32 v[34:35], v[30:31], v[54:55], v[34:35] op_sel_hi:[0,1,1] neg_lo:[1,0,0] neg_hi:[1,0,0]
	v_pk_add_f32 v[30:31], v[56:57], v[58:59]
	v_pk_add_f32 v[54:55], v[56:57], v[58:59] neg_lo:[0,1] neg_hi:[0,1]
	v_pk_add_f32 v[56:57], v[52:53], v[36:37]
	v_pk_add_f32 v[36:37], v[36:37], v[52:53] neg_lo:[0,1] neg_hi:[0,1]
	v_pk_mul_f32 v[52:53], v[10:11], v[36:37] op_sel:[0,1] op_sel_hi:[0,0] neg_lo:[1,1] neg_hi:[1,0]
	v_pk_fma_f32 v[58:59], v[10:11], v[36:37], v[52:53] op_sel_hi:[0,1,1]
	v_pk_add_f32 v[52:53], v[60:61], v[72:73] neg_lo:[0,1] neg_hi:[0,1]
	v_pk_add_f32 v[36:37], v[60:61], v[72:73]
	v_xor_b32_e32 v61, 0x80000000, v52
	v_mov_b32_e32 v60, v53
	v_pk_add_f32 v[52:53], v[46:47], v[68:69]
	v_pk_add_f32 v[46:47], v[46:47], v[68:69] neg_lo:[0,1] neg_hi:[0,1]
	v_pk_add_f32 v[72:73], v[64:65], v[40:41]
	v_pk_add_f32 v[40:41], v[40:41], v[64:65] neg_lo:[0,1] neg_hi:[0,1]
	v_pk_mul_f32 v[68:69], v[10:11], v[46:47] op_sel:[0,1] op_sel_hi:[0,0] neg_lo:[1,1] neg_hi:[1,0]
	v_pk_fma_f32 v[46:47], v[10:11], v[46:47], v[68:69] op_sel_hi:[0,1,1] neg_lo:[1,0,0] neg_hi:[1,0,0]
	v_pk_add_f32 v[68:69], v[30:31], v[36:37]
	v_pk_add_f32 v[30:31], v[30:31], v[36:37] neg_lo:[0,1] neg_hi:[0,1]
	v_pk_add_f32 v[36:37], v[56:57], v[52:53]
	v_pk_add_f32 v[52:53], v[56:57], v[52:53] neg_lo:[0,1] neg_hi:[0,1]
	v_pk_mul_f32 v[64:65], v[10:11], v[40:41] op_sel:[0,1] op_sel_hi:[0,0] neg_lo:[1,1] neg_hi:[1,0]
	v_xor_b32_e32 v57, 0x80000000, v52
	v_mov_b32_e32 v56, v53
	v_pk_fma_f32 v[64:65], v[10:11], v[40:41], v[64:65] op_sel_hi:[0,1,1]
	v_pk_add_f32 v[40:41], v[62:63], v[66:67]
	v_pk_add_f32 v[62:63], v[62:63], v[66:67] neg_lo:[0,1] neg_hi:[0,1]
	v_pk_add_f32 v[70:71], v[68:69], v[36:37]
	v_pk_add_f32 v[52:53], v[68:69], v[36:37] neg_lo:[0,1] neg_hi:[0,1]
	v_pk_add_f32 v[68:69], v[30:31], v[56:57]
	v_pk_add_f32 v[36:37], v[30:31], v[56:57] neg_lo:[0,1] neg_hi:[0,1]
	v_pk_add_f32 v[56:57], v[58:59], v[46:47]
	v_pk_add_f32 v[46:47], v[58:59], v[46:47] neg_lo:[0,1] neg_hi:[0,1]
	v_xor_b32_e32 v67, 0x80000000, v62
	v_mov_b32_e32 v66, v63
	v_pk_add_f32 v[62:63], v[50:51], v[34:35]
	v_pk_add_f32 v[34:35], v[50:51], v[34:35] neg_lo:[0,1] neg_hi:[0,1]
	v_pk_add_f32 v[30:31], v[54:55], v[60:61]
	v_pk_add_f32 v[54:55], v[54:55], v[60:61] neg_lo:[0,1] neg_hi:[0,1]
	v_xor_b32_e32 v59, 0x80000000, v46
	v_mov_b32_e32 v58, v47
	v_pk_add_f32 v[60:61], v[30:31], v[56:57]
	v_pk_add_f32 v[46:47], v[30:31], v[56:57] neg_lo:[0,1] neg_hi:[0,1]
	v_pk_add_f32 v[56:57], v[54:55], v[58:59]
	v_pk_add_f32 v[30:31], v[54:55], v[58:59] neg_lo:[0,1] neg_hi:[0,1]
	v_pk_add_f32 v[54:55], v[76:77], v[74:75]
	v_pk_mul_f32 v[50:51], v[10:11], v[34:35] op_sel:[0,1] op_sel_hi:[0,0] neg_lo:[1,1] neg_hi:[1,0]
	v_pk_add_f32 v[58:59], v[76:77], v[74:75] neg_lo:[0,1] neg_hi:[0,1]
	v_pk_fma_f32 v[34:35], v[10:11], v[34:35], v[50:51] op_sel_hi:[0,1,1] neg_lo:[1,0,0] neg_hi:[1,0,0]
	v_pk_add_f32 v[50:51], v[54:55], v[40:41]
	v_pk_add_f32 v[40:41], v[54:55], v[40:41] neg_lo:[0,1] neg_hi:[0,1]
	v_pk_add_f32 v[54:55], v[72:73], v[62:63]
	v_pk_add_f32 v[62:63], v[72:73], v[62:63] neg_lo:[0,1] neg_hi:[0,1]
	v_lshl_add_u32 v10, v13, 3, 0
	v_xor_b32_e32 v73, 0x80000000, v62
	v_mov_b32_e32 v72, v63
	v_pk_add_f32 v[62:63], v[50:51], v[54:55]
	v_pk_add_f32 v[54:55], v[50:51], v[54:55] neg_lo:[0,1] neg_hi:[0,1]
	v_pk_add_f32 v[50:51], v[58:59], v[66:67]
	v_pk_add_f32 v[58:59], v[58:59], v[66:67] neg_lo:[0,1] neg_hi:[0,1]
	v_pk_add_f32 v[66:67], v[64:65], v[34:35]
	v_pk_add_f32 v[34:35], v[64:65], v[34:35] neg_lo:[0,1] neg_hi:[0,1]
	v_pk_add_f32 v[74:75], v[40:41], v[72:73]
	v_pk_add_f32 v[40:41], v[40:41], v[72:73] neg_lo:[0,1] neg_hi:[0,1]
	v_pk_add_f32 v[72:73], v[50:51], v[66:67]
	v_pk_add_f32 v[50:51], v[50:51], v[66:67] neg_lo:[0,1] neg_hi:[0,1]
	v_pk_add_f32 v[66:67], v[58:59], v[34:35] op_sel:[0,1] op_sel_hi:[1,0] neg_hi:[0,1]
	v_pk_add_f32 v[34:35], v[58:59], v[34:35] op_sel:[0,1] op_sel_hi:[1,0] neg_lo:[0,1]
	v_pk_mul_f32 v[58:59], v[84:85], s[14:15] op_sel:[1,0] neg_lo:[1,0]
	v_pk_fma_f32 v[58:59], v[84:85], s[94:95], v[58:59] op_sel_hi:[0,1,1]
	ds_write_b64 v10, v[58:59]
	v_pk_fma_f32 v[58:59], v[178:179], s[90:91], v[178:179] op_sel:[1,0,0] op_sel_hi:[0,1,1]
	v_pk_mul_f32 v[64:65], v[58:59], v[70:71] op_sel:[1,1] op_sel_hi:[0,1] neg_lo:[0,1]
	v_pk_fma_f32 v[64:65], v[58:59], v[70:71], v[64:65] op_sel_hi:[1,0,1]
	ds_write_b64 v10, v[64:65] offset:4224
	v_pk_mul_f32 v[64:65], v[178:179], v[58:59] op_sel:[1,1] op_sel_hi:[0,1] neg_lo:[0,1]
	v_pk_fma_f32 v[58:59], v[178:179], v[58:59], v[64:65] op_sel_hi:[1,0,1]
	v_pk_mul_f32 v[64:65], v[58:59], v[88:89] op_sel:[1,1] op_sel_hi:[0,1] neg_lo:[0,1]
	v_pk_fma_f32 v[64:65], v[58:59], v[88:89], v[64:65] op_sel_hi:[1,0,1]
	ds_write_b64 v10, v[64:65] offset:8448
	v_pk_mul_f32 v[64:65], v[178:179], v[58:59] op_sel:[1,1] op_sel_hi:[0,1] neg_lo:[0,1]
	v_pk_fma_f32 v[58:59], v[178:179], v[58:59], v[64:65] op_sel_hi:[1,0,1]
	v_pk_mul_f32 v[64:65], v[58:59], v[62:63] op_sel:[1,1] op_sel_hi:[0,1] neg_lo:[0,1]
	v_pk_fma_f32 v[62:63], v[58:59], v[62:63], v[64:65] op_sel_hi:[1,0,1]
	ds_write_b64 v10, v[62:63] offset:12672
	v_pk_mul_f32 v[62:63], v[178:179], v[58:59] op_sel:[1,1] op_sel_hi:[0,1] neg_lo:[0,1]
	v_pk_fma_f32 v[58:59], v[178:179], v[58:59], v[62:63] op_sel_hi:[1,0,1]
	v_pk_mul_f32 v[62:63], v[58:59], v[78:79] op_sel:[1,1] op_sel_hi:[0,1] neg_lo:[0,1]
	v_pk_fma_f32 v[62:63], v[58:59], v[78:79], v[62:63] op_sel_hi:[1,0,1]
	ds_write_b64 v10, v[62:63] offset:16896
	v_pk_mul_f32 v[62:63], v[178:179], v[58:59] op_sel:[1,1] op_sel_hi:[0,1] neg_lo:[0,1]
	v_pk_fma_f32 v[58:59], v[178:179], v[58:59], v[62:63] op_sel_hi:[1,0,1]
	v_pk_mul_f32 v[62:63], v[58:59], v[60:61] op_sel:[1,1] op_sel_hi:[0,1] neg_lo:[0,1]
	v_pk_fma_f32 v[60:61], v[58:59], v[60:61], v[62:63] op_sel_hi:[1,0,1]
	ds_write_b64 v10, v[60:61] offset:21120
	v_pk_mul_f32 v[60:61], v[178:179], v[58:59] op_sel:[1,1] op_sel_hi:[0,1] neg_lo:[0,1]
	v_pk_fma_f32 v[58:59], v[178:179], v[58:59], v[60:61] op_sel_hi:[1,0,1]
	v_pk_mul_f32 v[60:61], v[82:83], v[58:59] op_sel:[1,1] op_sel_hi:[1,0] neg_lo:[1,0]
	v_pk_fma_f32 v[60:61], v[82:83], v[58:59], v[60:61] op_sel_hi:[0,1,1]
	ds_write_b64 v10, v[60:61] offset:25344
	v_pk_mul_f32 v[60:61], v[178:179], v[58:59] op_sel:[1,1] op_sel_hi:[0,1] neg_lo:[0,1]
	v_pk_fma_f32 v[58:59], v[178:179], v[58:59], v[60:61] op_sel_hi:[1,0,1]
	v_pk_mul_f32 v[60:61], v[72:73], v[58:59] op_sel:[1,1] op_sel_hi:[1,0] neg_lo:[1,0]
	v_pk_fma_f32 v[60:61], v[72:73], v[58:59], v[60:61] op_sel_hi:[0,1,1]
	ds_write_b64 v10, v[60:61] offset:29568
	v_pk_mul_f32 v[60:61], v[178:179], v[58:59] op_sel:[1,1] op_sel_hi:[0,1] neg_lo:[0,1]
	v_pk_fma_f32 v[58:59], v[178:179], v[58:59], v[60:61] op_sel_hi:[1,0,1]
	v_pk_mul_f32 v[60:61], v[44:45], v[58:59] op_sel:[1,1] op_sel_hi:[1,0] neg_lo:[1,0]
	v_pk_fma_f32 v[44:45], v[44:45], v[58:59], v[60:61] op_sel_hi:[0,1,1]
	ds_write_b64 v10, v[44:45] offset:33792
	v_pk_mul_f32 v[44:45], v[178:179], v[58:59] op_sel:[1,1] op_sel_hi:[0,1] neg_lo:[0,1]
	v_pk_fma_f32 v[44:45], v[178:179], v[58:59], v[44:45] op_sel_hi:[1,0,1]
	v_pk_mul_f32 v[58:59], v[68:69], v[44:45] op_sel:[1,1] op_sel_hi:[1,0] neg_lo:[1,0]
	v_pk_fma_f32 v[58:59], v[68:69], v[44:45], v[58:59] op_sel_hi:[0,1,1]
	ds_write_b64 v10, v[58:59] offset:38016
	v_pk_mul_f32 v[58:59], v[178:179], v[44:45] op_sel:[1,1] op_sel_hi:[0,1] neg_lo:[0,1]
	v_pk_fma_f32 v[44:45], v[178:179], v[44:45], v[58:59] op_sel_hi:[1,0,1]
	v_pk_mul_f32 v[58:59], v[48:49], v[44:45] op_sel:[1,1] op_sel_hi:[1,0] neg_lo:[1,0]
	v_pk_fma_f32 v[48:49], v[48:49], v[44:45], v[58:59] op_sel_hi:[0,1,1]
	ds_write_b64 v10, v[48:49] offset:42240
	v_pk_mul_f32 v[48:49], v[178:179], v[44:45] op_sel:[1,1] op_sel_hi:[0,1] neg_lo:[0,1]
	v_pk_fma_f32 v[44:45], v[178:179], v[44:45], v[48:49] op_sel_hi:[1,0,1]
	v_pk_mul_f32 v[48:49], v[74:75], v[44:45] op_sel:[1,1] op_sel_hi:[1,0] neg_lo:[1,0]
	v_pk_fma_f32 v[48:49], v[74:75], v[44:45], v[48:49] op_sel_hi:[0,1,1]
	ds_write_b64 v10, v[48:49] offset:46464
	v_pk_mul_f32 v[48:49], v[178:179], v[44:45] op_sel:[1,1] op_sel_hi:[0,1] neg_lo:[0,1]
	v_pk_fma_f32 v[44:45], v[178:179], v[44:45], v[48:49] op_sel_hi:[1,0,1]
	v_pk_mul_f32 v[48:49], v[38:39], v[44:45] op_sel:[1,1] op_sel_hi:[1,0] neg_lo:[1,0]
	v_pk_fma_f32 v[38:39], v[38:39], v[44:45], v[48:49] op_sel_hi:[0,1,1]
	ds_write_b64 v10, v[38:39] offset:50688
	v_pk_mul_f32 v[38:39], v[178:179], v[44:45] op_sel:[1,1] op_sel_hi:[0,1] neg_lo:[0,1]
	v_pk_fma_f32 v[38:39], v[178:179], v[44:45], v[38:39] op_sel_hi:[1,0,1]
	v_pk_mul_f32 v[44:45], v[56:57], v[38:39] op_sel:[1,1] op_sel_hi:[1,0] neg_lo:[1,0]
	v_pk_fma_f32 v[44:45], v[56:57], v[38:39], v[44:45] op_sel_hi:[0,1,1]
	ds_write_b64 v10, v[44:45] offset:54912
	v_pk_mul_f32 v[44:45], v[178:179], v[38:39] op_sel:[1,1] op_sel_hi:[0,1] neg_lo:[0,1]
	v_pk_fma_f32 v[38:39], v[178:179], v[38:39], v[44:45] op_sel_hi:[1,0,1]
	v_pk_mul_f32 v[44:45], v[42:43], v[38:39] op_sel:[1,1] op_sel_hi:[1,0] neg_lo:[1,0]
	v_pk_fma_f32 v[42:43], v[42:43], v[38:39], v[44:45] op_sel_hi:[0,1,1]
	ds_write_b64 v10, v[42:43] offset:59136
	v_pk_mul_f32 v[42:43], v[178:179], v[38:39] op_sel:[1,1] op_sel_hi:[0,1] neg_lo:[0,1]
	v_pk_fma_f32 v[38:39], v[178:179], v[38:39], v[42:43] op_sel_hi:[1,0,1]
	v_pk_mul_f32 v[42:43], v[66:67], v[38:39] op_sel:[1,1] op_sel_hi:[1,0] neg_lo:[1,0]
	v_pk_fma_f32 v[42:43], v[66:67], v[38:39], v[42:43] op_sel_hi:[0,1,1]
	ds_write_b64 v10, v[42:43] offset:63360
	v_pk_mul_f32 v[42:43], v[178:179], v[38:39] op_sel:[1,1] op_sel_hi:[0,1] neg_lo:[0,1]
	v_pk_fma_f32 v[38:39], v[178:179], v[38:39], v[42:43] op_sel_hi:[1,0,1]
	v_pk_mul_f32 v[42:43], v[28:29], v[38:39] op_sel:[1,1] op_sel_hi:[1,0] neg_lo:[1,0]
	v_add_u32_e32 v13, 0x10800, v10
	v_pk_fma_f32 v[28:29], v[28:29], v[38:39], v[42:43] op_sel_hi:[0,1,1]
	ds_write_b64 v13, v[28:29]
	v_pk_mul_f32 v[28:29], v[178:179], v[38:39] op_sel:[1,1] op_sel_hi:[0,1] neg_lo:[0,1]
	v_pk_fma_f32 v[28:29], v[178:179], v[38:39], v[28:29] op_sel_hi:[1,0,1]
	v_pk_mul_f32 v[38:39], v[52:53], v[28:29] op_sel:[1,1] op_sel_hi:[1,0] neg_lo:[1,0]
	v_add_u32_e32 v13, 0x11880, v10
	v_pk_fma_f32 v[38:39], v[52:53], v[28:29], v[38:39] op_sel_hi:[0,1,1]
	ds_write_b64 v13, v[38:39]
	v_pk_mul_f32 v[38:39], v[178:179], v[28:29] op_sel:[1,1] op_sel_hi:[0,1] neg_lo:[0,1]
	v_pk_fma_f32 v[28:29], v[178:179], v[28:29], v[38:39] op_sel_hi:[1,0,1]
	v_pk_mul_f32 v[38:39], v[32:33], v[28:29] op_sel:[1,1] op_sel_hi:[1,0] neg_lo:[1,0]
	v_add_u32_e32 v13, 0x12900, v10
	v_pk_fma_f32 v[32:33], v[32:33], v[28:29], v[38:39] op_sel_hi:[0,1,1]
	ds_write_b64 v13, v[32:33]
	v_pk_mul_f32 v[32:33], v[178:179], v[28:29] op_sel:[1,1] op_sel_hi:[0,1] neg_lo:[0,1]
	v_pk_fma_f32 v[28:29], v[178:179], v[28:29], v[32:33] op_sel_hi:[1,0,1]
	v_pk_mul_f32 v[32:33], v[54:55], v[28:29] op_sel:[1,1] op_sel_hi:[1,0] neg_lo:[1,0]
	v_add_u32_e32 v13, 0x13980, v10
	v_pk_fma_f32 v[32:33], v[54:55], v[28:29], v[32:33] op_sel_hi:[0,1,1]
	ds_write_b64 v13, v[32:33]
	v_pk_mul_f32 v[32:33], v[178:179], v[28:29] op_sel:[1,1] op_sel_hi:[0,1] neg_lo:[0,1]
	v_pk_fma_f32 v[28:29], v[178:179], v[28:29], v[32:33] op_sel_hi:[1,0,1]
	v_pk_mul_f32 v[32:33], v[24:25], v[28:29] op_sel:[1,1] op_sel_hi:[1,0] neg_lo:[1,0]
	v_add_u32_e32 v13, 0x14a00, v10
	v_pk_fma_f32 v[24:25], v[24:25], v[28:29], v[32:33] op_sel_hi:[0,1,1]
	ds_write_b64 v13, v[24:25]
	v_pk_mul_f32 v[24:25], v[178:179], v[28:29] op_sel:[1,1] op_sel_hi:[0,1] neg_lo:[0,1]
	v_pk_fma_f32 v[24:25], v[178:179], v[28:29], v[24:25] op_sel_hi:[1,0,1]
	v_pk_mul_f32 v[28:29], v[46:47], v[24:25] op_sel:[1,1] op_sel_hi:[1,0] neg_lo:[1,0]
	v_add_u32_e32 v13, 0x15a80, v10
	v_pk_fma_f32 v[28:29], v[46:47], v[24:25], v[28:29] op_sel_hi:[0,1,1]
	ds_write_b64 v13, v[28:29]
	v_pk_mul_f32 v[28:29], v[178:179], v[24:25] op_sel:[1,1] op_sel_hi:[0,1] neg_lo:[0,1]
	v_pk_fma_f32 v[24:25], v[178:179], v[24:25], v[28:29] op_sel_hi:[1,0,1]
	v_pk_mul_f32 v[28:29], v[26:27], v[24:25] op_sel:[1,1] op_sel_hi:[1,0] neg_lo:[1,0]
	v_add_u32_e32 v13, 0x16b00, v10
	v_pk_fma_f32 v[26:27], v[26:27], v[24:25], v[28:29] op_sel_hi:[0,1,1]
	ds_write_b64 v13, v[26:27]
	v_pk_mul_f32 v[26:27], v[178:179], v[24:25] op_sel:[1,1] op_sel_hi:[0,1] neg_lo:[0,1]
	v_pk_fma_f32 v[24:25], v[178:179], v[24:25], v[26:27] op_sel_hi:[1,0,1]
	v_pk_mul_f32 v[26:27], v[50:51], v[24:25] op_sel:[1,1] op_sel_hi:[1,0] neg_lo:[1,0]
	v_add_u32_e32 v13, 0x17b80, v10
	v_pk_fma_f32 v[26:27], v[50:51], v[24:25], v[26:27] op_sel_hi:[0,1,1]
	ds_write_b64 v13, v[26:27]
	v_pk_mul_f32 v[26:27], v[178:179], v[24:25] op_sel:[1,1] op_sel_hi:[0,1] neg_lo:[0,1]
	v_pk_fma_f32 v[24:25], v[178:179], v[24:25], v[26:27] op_sel_hi:[1,0,1]
	v_pk_mul_f32 v[26:27], v[20:21], v[24:25] op_sel:[1,1] op_sel_hi:[1,0] neg_lo:[1,0]
	v_add_u32_e32 v13, 0x18c00, v10
	v_pk_fma_f32 v[20:21], v[20:21], v[24:25], v[26:27] op_sel_hi:[0,1,1]
	ds_write_b64 v13, v[20:21]
	v_pk_mul_f32 v[20:21], v[178:179], v[24:25] op_sel:[1,1] op_sel_hi:[0,1] neg_lo:[0,1]
	v_pk_fma_f32 v[20:21], v[178:179], v[24:25], v[20:21] op_sel_hi:[1,0,1]
	v_pk_mul_f32 v[24:25], v[36:37], v[20:21] op_sel:[1,1] op_sel_hi:[1,0] neg_lo:[1,0]
	v_add_u32_e32 v13, 0x19c80, v10
	v_pk_fma_f32 v[24:25], v[36:37], v[20:21], v[24:25] op_sel_hi:[0,1,1]
	ds_write_b64 v13, v[24:25]
	v_pk_mul_f32 v[24:25], v[178:179], v[20:21] op_sel:[1,1] op_sel_hi:[0,1] neg_lo:[0,1]
	v_pk_fma_f32 v[20:21], v[178:179], v[20:21], v[24:25] op_sel_hi:[1,0,1]
	v_pk_mul_f32 v[24:25], v[22:23], v[20:21] op_sel:[1,1] op_sel_hi:[1,0] neg_lo:[1,0]
	v_add_u32_e32 v13, 0x1ad00, v10
	v_pk_fma_f32 v[22:23], v[22:23], v[20:21], v[24:25] op_sel_hi:[0,1,1]
	ds_write_b64 v13, v[22:23]
	v_pk_mul_f32 v[22:23], v[178:179], v[20:21] op_sel:[1,1] op_sel_hi:[0,1] neg_lo:[0,1]
	v_pk_fma_f32 v[20:21], v[178:179], v[20:21], v[22:23] op_sel_hi:[1,0,1]
	v_pk_mul_f32 v[22:23], v[40:41], v[20:21] op_sel:[1,1] op_sel_hi:[1,0] neg_lo:[1,0]
	v_add_u32_e32 v13, 0x1bd80, v10
	v_pk_fma_f32 v[22:23], v[40:41], v[20:21], v[22:23] op_sel_hi:[0,1,1]
	ds_write_b64 v13, v[22:23]
	v_pk_mul_f32 v[22:23], v[178:179], v[20:21] op_sel:[1,1] op_sel_hi:[0,1] neg_lo:[0,1]
	v_pk_fma_f32 v[20:21], v[178:179], v[20:21], v[22:23] op_sel_hi:[1,0,1]
	v_pk_mul_f32 v[22:23], v[16:17], v[20:21] op_sel:[1,1] op_sel_hi:[1,0] neg_lo:[1,0]
	v_add_u32_e32 v13, 0x1ce00, v10
	v_pk_fma_f32 v[16:17], v[16:17], v[20:21], v[22:23] op_sel_hi:[0,1,1]
	ds_write_b64 v13, v[16:17]
	v_pk_mul_f32 v[16:17], v[178:179], v[20:21] op_sel:[1,1] op_sel_hi:[0,1] neg_lo:[0,1]
	v_pk_fma_f32 v[16:17], v[178:179], v[20:21], v[16:17] op_sel_hi:[1,0,1]
	v_pk_mul_f32 v[20:21], v[30:31], v[16:17] op_sel:[1,1] op_sel_hi:[1,0] neg_lo:[1,0]
	v_add_u32_e32 v13, 0x1de80, v10
	v_pk_fma_f32 v[20:21], v[30:31], v[16:17], v[20:21] op_sel_hi:[0,1,1]
	ds_write_b64 v13, v[20:21]
	v_pk_mul_f32 v[20:21], v[178:179], v[16:17] op_sel:[1,1] op_sel_hi:[0,1] neg_lo:[0,1]
	v_pk_fma_f32 v[16:17], v[178:179], v[16:17], v[20:21] op_sel_hi:[1,0,1]
	v_pk_mul_f32 v[20:21], v[18:19], v[16:17] op_sel:[1,1] op_sel_hi:[1,0] neg_lo:[1,0]
	v_add_u32_e32 v13, 0x1ef00, v10
	v_pk_fma_f32 v[18:19], v[18:19], v[16:17], v[20:21] op_sel_hi:[0,1,1]
	ds_write_b64 v13, v[18:19]
	v_pk_mul_f32 v[18:19], v[178:179], v[16:17] op_sel:[1,1] op_sel_hi:[0,1] neg_lo:[0,1]
	v_pk_fma_f32 v[14:15], v[178:179], v[16:17], v[18:19] op_sel_hi:[1,0,1]
	v_pk_mul_f32 v[16:17], v[34:35], v[14:15] op_sel:[1,1] op_sel_hi:[1,0] neg_lo:[1,0]
	v_add_u32_e32 v10, 0x1ff80, v10
	v_pk_fma_f32 v[14:15], v[34:35], v[14:15], v[16:17] op_sel_hi:[0,1,1]
	ds_write_b64 v10, v[14:15]
	v_mov_b32_e32 v10, v174
	v_mov_b32_e32 v13, v172
	s_waitcnt lgkmcnt(0)
	s_barrier
	v_mov_b32_e32 v14, v180
	v_xad_u32 v28, v13, 3, v10
	v_lshl_add_u32 v71, v28, 3, 0
	v_xad_u32 v28, v13, 4, v10
	v_lshl_add_u32 v70, v28, 3, 0
	v_xad_u32 v28, v13, 5, v10
	v_lshl_add_u32 v69, v28, 3, 0
	v_xad_u32 v28, v13, 6, v10
	v_lshl_add_u32 v68, v28, 3, 0
	v_xad_u32 v28, v13, 7, v10
	v_lshl_add_u32 v67, v28, 3, 0
	v_xad_u32 v28, v13, 8, v10
	v_lshl_add_u32 v28, v28, 3, 0
	v_add_u32_e32 v66, 0x800, v28
	v_xad_u32 v28, v13, 9, v10
	v_lshl_add_u32 v28, v28, 3, 0
	v_add_u32_e32 v65, 0x800, v28
	v_xad_u32 v28, v13, 10, v10
	v_lshl_add_u32 v28, v28, 3, 0
	v_add_u32_e32 v64, 0x800, v28
	v_xad_u32 v28, v13, 11, v10
	v_lshl_add_u32 v28, v28, 3, 0
	v_add_u32_e32 v16, v13, v10
	v_add_u32_e32 v63, 0x800, v28
	v_xad_u32 v28, v13, 12, v10
	v_mov_b32_e32 v15, v181
	v_lshl_add_u32 v74, v16, 3, 0
	v_lshl_add_u32 v28, v28, 3, 0
	ds_read2_b64 v[16:19], v74 offset1:16
	ds_read2_b64 v[38:41], v66 offset1:16
	v_add_u32_e32 v62, 0x800, v28
	v_xad_u32 v28, v13, 13, v10
	v_xad_u32 v20, v13, 1, v10
	v_lshl_add_u32 v28, v28, 3, 0
	v_lshl_add_u32 v73, v20, 3, 0
	v_xad_u32 v24, v13, 2, v10
	v_add_u32_e32 v61, 0x800, v28
	v_xad_u32 v28, v13, 14, v10
	v_xad_u32 v10, v13, 15, v10
	ds_read2_b64 v[20:23], v73 offset0:32 offset1:48
	ds_read2_b64 v[46:49], v65 offset0:32 offset1:48
	v_lshl_add_u32 v28, v28, 3, 0
	v_lshl_add_u32 v10, v10, 3, 0
	v_lshl_add_u32 v72, v24, 3, 0
	v_add_u32_e32 v60, 0x800, v28
	v_add_u32_e32 v13, 0x800, v10
	v_mov_b32_e32 v10, v1
	ds_read2_b64 v[24:27], v72 offset0:64 offset1:80
	ds_read2_b64 v[56:59], v71 offset0:96 offset1:112
	ds_read2_b64 v[76:79], v70 offset0:128 offset1:144
	ds_read2_b64 v[80:83], v69 offset0:160 offset1:176
	ds_read2_b64 v[84:87], v68 offset0:192 offset1:208
	ds_read2_b64 v[88:91], v67 offset0:224 offset1:240
	ds_read2_b64 v[52:55], v64 offset0:64 offset1:80
	ds_read2_b64 v[92:95], v63 offset0:96 offset1:112
	ds_read2_b64 v[96:99], v62 offset0:128 offset1:144
	ds_read2_b64 v[100:103], v61 offset0:160 offset1:176
	ds_read2_b64 v[104:107], v60 offset0:192 offset1:208
	ds_read2_b64 v[108:111], v13 offset0:224 offset1:240
	s_waitcnt lgkmcnt(14)
	v_pk_add_f32 v[112:113], v[16:17], v[38:39]
	v_pk_add_f32 v[38:39], v[16:17], v[38:39] neg_lo:[0,1] neg_hi:[0,1]
	v_pk_add_f32 v[16:17], v[18:19], v[40:41]
	v_pk_add_f32 v[18:19], v[18:19], v[40:41] neg_lo:[0,1] neg_hi:[0,1]
	v_mov_b32_e32 v28, v164
	v_mov_b32_e32 v30, v165
	v_mov_b32_e32 v32, v166
	v_mov_b32_e32 v10, v167
	v_mov_b32_e32 v36, v168
	v_mov_b32_e32 v34, v169
	v_mov_b32_e32 v44, v170
	v_mov_b32_e32 v29, v171
	v_pk_mul_f32 v[40:41], v[18:19], v[44:45] op_sel:[1,0] op_sel_hi:[0,0] neg_lo:[1,1] neg_hi:[0,1]
	v_pk_fma_f32 v[42:43], v[18:19], v[28:29], v[40:41] op_sel_hi:[1,0,1]
	s_waitcnt lgkmcnt(12)
	v_pk_add_f32 v[18:19], v[20:21], v[46:47]
	v_pk_add_f32 v[20:21], v[20:21], v[46:47] neg_lo:[0,1] neg_hi:[0,1]
	v_pk_mul_f32 v[40:41], v[20:21], v[34:35] op_sel:[1,0] op_sel_hi:[0,0] neg_lo:[1,1] neg_hi:[0,1]
	v_pk_fma_f32 v[46:47], v[20:21], v[30:31], v[40:41] op_sel_hi:[1,0,1]
	v_pk_add_f32 v[20:21], v[22:23], v[48:49]
	v_pk_add_f32 v[22:23], v[22:23], v[48:49] neg_lo:[0,1] neg_hi:[0,1]
	v_pk_mul_f32 v[40:41], v[22:23], v[36:37] op_sel:[1,0] op_sel_hi:[0,0] neg_lo:[1,1] neg_hi:[0,1]
	v_pk_fma_f32 v[50:51], v[22:23], v[32:33], v[40:41] op_sel_hi:[1,0,1]
	s_waitcnt lgkmcnt(5)
	v_pk_add_f32 v[22:23], v[24:25], v[52:53]
	v_pk_add_f32 v[24:25], v[24:25], v[52:53] neg_lo:[0,1] neg_hi:[0,1]
	v_pk_mul_f32 v[40:41], v[24:25], v[10:11] op_sel:[1,0] op_sel_hi:[0,0] neg_lo:[1,1] neg_hi:[0,1]
	v_pk_fma_f32 v[52:53], v[24:25], v[10:11], v[40:41] op_sel_hi:[1,0,1]
	v_pk_add_f32 v[24:25], v[26:27], v[54:55]
	v_pk_add_f32 v[26:27], v[26:27], v[54:55] neg_lo:[0,1] neg_hi:[0,1]
	v_pk_mul_f32 v[40:41], v[26:27], v[36:37] op_sel_hi:[1,0]
	v_pk_fma_f32 v[54:55], v[26:27], v[32:33], v[40:41] op_sel:[1,0,0] op_sel_hi:[0,0,1] neg_lo:[1,1,0] neg_hi:[0,1,0]
	s_waitcnt lgkmcnt(4)
	v_pk_add_f32 v[40:41], v[56:57], v[92:93] neg_lo:[0,1] neg_hi:[0,1]
	v_pk_add_f32 v[26:27], v[56:57], v[92:93]
	v_pk_mul_f32 v[48:49], v[40:41], v[34:35] op_sel_hi:[1,0]
	v_pk_fma_f32 v[56:57], v[40:41], v[30:31], v[48:49] op_sel:[1,0,0] op_sel_hi:[0,0,1] neg_lo:[1,1,0] neg_hi:[0,1,0]
	v_pk_add_f32 v[48:49], v[58:59], v[94:95] neg_lo:[0,1] neg_hi:[0,1]
	v_pk_add_f32 v[40:41], v[58:59], v[94:95]
	v_pk_mul_f32 v[58:59], v[48:49], v[44:45] op_sel_hi:[1,0]
	v_xor_b32_e32 v92, 0x80000000, v49
	v_mov_b32_e32 v93, v48
	s_waitcnt lgkmcnt(3)
	v_pk_add_f32 v[48:49], v[76:77], v[96:97]
	v_pk_add_f32 v[76:77], v[76:77], v[96:97] neg_lo:[0,1] neg_hi:[0,1]
	v_pk_fma_f32 v[58:59], v[92:93], v[28:29], v[58:59] op_sel_hi:[1,0,1] neg_lo:[0,1,0] neg_hi:[0,1,0]
	v_xor_b32_e32 v93, 0x80000000, v76
	v_mov_b32_e32 v92, v77
	v_pk_add_f32 v[76:77], v[78:79], v[98:99]
	v_pk_add_f32 v[78:79], v[78:79], v[98:99] neg_lo:[0,1] neg_hi:[0,1]
	v_pk_mul_f32 v[94:95], v[78:79], v[44:45] op_sel_hi:[1,0] neg_lo:[0,1] neg_hi:[0,1]
	v_pk_fma_f32 v[78:79], v[78:79], v[28:29], v[94:95] op_sel:[1,0,0] op_sel_hi:[0,0,1] neg_lo:[1,1,0] neg_hi:[0,1,0]
	s_waitcnt lgkmcnt(2)
	v_pk_add_f32 v[94:95], v[80:81], v[100:101]
	v_pk_add_f32 v[80:81], v[80:81], v[100:101] neg_lo:[0,1] neg_hi:[0,1]
	v_pk_mul_f32 v[96:97], v[80:81], v[34:35] op_sel_hi:[1,0] neg_lo:[0,1] neg_hi:[0,1]
	v_pk_fma_f32 v[80:81], v[80:81], v[30:31], v[96:97] op_sel:[1,0,0] op_sel_hi:[0,0,1] neg_lo:[1,1,0] neg_hi:[0,1,0]
	v_pk_add_f32 v[96:97], v[82:83], v[102:103]
	v_pk_add_f32 v[82:83], v[82:83], v[102:103] neg_lo:[0,1] neg_hi:[0,1]
	v_pk_mul_f32 v[98:99], v[82:83], v[36:37] op_sel_hi:[1,0] neg_lo:[0,1] neg_hi:[0,1]
	v_pk_fma_f32 v[82:83], v[82:83], v[32:33], v[98:99] op_sel:[1,0,0] op_sel_hi:[0,0,1] neg_lo:[1,1,0] neg_hi:[0,1,0]
	s_waitcnt lgkmcnt(1)
	v_pk_add_f32 v[98:99], v[84:85], v[104:105]
	v_pk_add_f32 v[84:85], v[84:85], v[104:105] neg_lo:[0,1] neg_hi:[0,1]
	v_pk_mul_f32 v[100:101], v[84:85], v[10:11] op_sel:[1,0] op_sel_hi:[0,0] neg_lo:[1,1] neg_hi:[0,1]
	v_pk_fma_f32 v[84:85], v[84:85], v[10:11], v[100:101] op_sel_hi:[1,0,1] neg_lo:[0,1,0] neg_hi:[0,1,0]
	v_pk_add_f32 v[100:101], v[86:87], v[106:107]
	v_pk_add_f32 v[86:87], v[86:87], v[106:107] neg_lo:[0,1] neg_hi:[0,1]
	v_pk_mul_f32 v[36:37], v[86:87], v[36:37] op_sel:[1,0] op_sel_hi:[0,0] neg_lo:[1,1] neg_hi:[0,1]
	v_pk_fma_f32 v[86:87], v[86:87], v[32:33], v[36:37] op_sel_hi:[1,0,1] neg_lo:[0,1,0] neg_hi:[0,1,0]
	s_waitcnt lgkmcnt(0)
	v_pk_add_f32 v[36:37], v[88:89], v[108:109] neg_lo:[0,1] neg_hi:[0,1]
	v_pk_add_f32 v[32:33], v[88:89], v[108:109]
	v_pk_mul_f32 v[88:89], v[36:37], v[34:35] op_sel:[1,0] op_sel_hi:[0,0] neg_lo:[1,1] neg_hi:[0,1]
	v_pk_fma_f32 v[88:89], v[36:37], v[30:31], v[88:89] op_sel_hi:[1,0,1] neg_lo:[0,1,0] neg_hi:[0,1,0]
	v_pk_add_f32 v[36:37], v[90:91], v[110:111]
	v_pk_add_f32 v[90:91], v[90:91], v[110:111] neg_lo:[0,1] neg_hi:[0,1]
	v_pk_mul_f32 v[44:45], v[90:91], v[44:45] op_sel:[1,0] op_sel_hi:[0,0] neg_lo:[1,1] neg_hi:[0,1]
	v_pk_fma_f32 v[90:91], v[90:91], v[28:29], v[44:45] op_sel_hi:[1,0,1] neg_lo:[0,1,0] neg_hi:[0,1,0]
	v_pk_add_f32 v[44:45], v[16:17], v[76:77]
	v_pk_add_f32 v[16:17], v[16:17], v[76:77] neg_lo:[0,1] neg_hi:[0,1]
	v_pk_add_f32 v[28:29], v[112:113], v[48:49]
	v_pk_mul_f32 v[76:77], v[16:17], v[34:35] op_sel:[1,0] op_sel_hi:[0,0] neg_lo:[1,1] neg_hi:[0,1]
	v_pk_add_f32 v[48:49], v[112:113], v[48:49] neg_lo:[0,1] neg_hi:[0,1]
	v_pk_fma_f32 v[76:77], v[16:17], v[30:31], v[76:77] op_sel_hi:[1,0,1]
	v_pk_add_f32 v[16:17], v[18:19], v[94:95]
	v_pk_add_f32 v[18:19], v[18:19], v[94:95] neg_lo:[0,1] neg_hi:[0,1]
	v_pk_mul_f32 v[94:95], v[18:19], v[10:11] op_sel:[1,0] op_sel_hi:[0,0] neg_lo:[1,1] neg_hi:[0,1]
	v_pk_fma_f32 v[18:19], v[18:19], v[10:11], v[94:95] op_sel_hi:[1,0,1]
	v_pk_add_f32 v[94:95], v[20:21], v[96:97]
	v_pk_add_f32 v[20:21], v[20:21], v[96:97] neg_lo:[0,1] neg_hi:[0,1]
	v_pk_mul_f32 v[96:97], v[20:21], v[34:35] op_sel_hi:[1,0]
	v_xor_b32_e32 v102, 0x80000000, v21
	v_mov_b32_e32 v103, v20
	v_pk_add_f32 v[20:21], v[22:23], v[98:99]
	v_pk_add_f32 v[22:23], v[22:23], v[98:99] neg_lo:[0,1] neg_hi:[0,1]
	v_pk_fma_f32 v[96:97], v[102:103], v[30:31], v[96:97] op_sel_hi:[1,0,1] neg_lo:[0,1,0] neg_hi:[0,1,0]
	v_xor_b32_e32 v99, 0x80000000, v22
	v_mov_b32_e32 v98, v23
	v_pk_add_f32 v[22:23], v[24:25], v[100:101]
	v_pk_add_f32 v[24:25], v[24:25], v[100:101] neg_lo:[0,1] neg_hi:[0,1]
	v_pk_mul_f32 v[100:101], v[24:25], v[34:35] op_sel_hi:[1,0] neg_lo:[0,1] neg_hi:[0,1]
	v_xor_b32_e32 v102, 0x80000000, v25
	v_mov_b32_e32 v103, v24
	v_pk_add_f32 v[24:25], v[26:27], v[32:33]
	v_pk_add_f32 v[26:27], v[26:27], v[32:33] neg_lo:[0,1] neg_hi:[0,1]
	v_pk_fma_f32 v[100:101], v[102:103], v[30:31], v[100:101] op_sel_hi:[1,0,1] neg_lo:[0,1,0] neg_hi:[0,1,0]
	v_pk_mul_f32 v[32:33], v[26:27], v[10:11] op_sel:[1,0] op_sel_hi:[0,0] neg_lo:[1,1] neg_hi:[0,1]
	v_pk_add_f32 v[102:103], v[28:29], v[20:21] neg_lo:[0,1] neg_hi:[0,1]
	v_pk_fma_f32 v[26:27], v[26:27], v[10:11], v[32:33] op_sel_hi:[1,0,1] neg_lo:[0,1,0] neg_hi:[0,1,0]
	v_pk_add_f32 v[32:33], v[40:41], v[36:37]
	v_pk_add_f32 v[36:37], v[40:41], v[36:37] neg_lo:[0,1] neg_hi:[0,1]
	v_pk_mul_f32 v[40:41], v[36:37], v[34:35] op_sel:[1,0] op_sel_hi:[0,0] neg_lo:[1,1] neg_hi:[0,1]
	v_pk_fma_f32 v[40:41], v[36:37], v[30:31], v[40:41] op_sel_hi:[1,0,1] neg_lo:[0,1,0] neg_hi:[0,1,0]
	v_pk_add_f32 v[36:37], v[28:29], v[20:21]
	v_pk_add_f32 v[20:21], v[44:45], v[22:23]
	v_pk_add_f32 v[22:23], v[44:45], v[22:23] neg_lo:[0,1] neg_hi:[0,1]
	v_pk_mul_f32 v[28:29], v[22:23], v[10:11] op_sel:[1,0] op_sel_hi:[0,0] neg_lo:[1,1] neg_hi:[0,1]
	v_pk_fma_f32 v[22:23], v[22:23], v[10:11], v[28:29] op_sel_hi:[1,0,1]
	v_pk_add_f32 v[28:29], v[16:17], v[24:25]
	v_pk_add_f32 v[16:17], v[16:17], v[24:25] neg_lo:[0,1] neg_hi:[0,1]
	v_xor_b32_e32 v25, 0x80000000, v16
	v_mov_b32_e32 v24, v17
	v_pk_add_f32 v[16:17], v[94:95], v[32:33]
	v_pk_add_f32 v[32:33], v[94:95], v[32:33] neg_lo:[0,1] neg_hi:[0,1]
	v_pk_mul_f32 v[44:45], v[32:33], v[10:11] op_sel:[1,0] op_sel_hi:[0,0] neg_lo:[1,1] neg_hi:[0,1]
	v_pk_fma_f32 v[32:33], v[32:33], v[10:11], v[44:45] op_sel_hi:[1,0,1] neg_lo:[0,1,0] neg_hi:[0,1,0]
	v_pk_add_f32 v[44:45], v[36:37], v[28:29]
	v_pk_add_f32 v[36:37], v[36:37], v[28:29] neg_lo:[0,1] neg_hi:[0,1]
	v_pk_add_f32 v[28:29], v[20:21], v[16:17]
	v_pk_add_f32 v[16:17], v[20:21], v[16:17] neg_lo:[0,1] neg_hi:[0,1]
	v_pk_add_f32 v[94:95], v[44:45], v[28:29]
	v_xor_b32_e32 v21, 0x80000000, v16
	v_mov_b32_e32 v20, v17
	v_pk_add_f32 v[16:17], v[102:103], v[24:25]
	v_pk_add_f32 v[102:103], v[102:103], v[24:25] neg_lo:[0,1] neg_hi:[0,1]
	v_pk_add_f32 v[24:25], v[22:23], v[32:33]
	v_pk_add_f32 v[22:23], v[22:23], v[32:33] neg_lo:[0,1] neg_hi:[0,1]
	v_pk_add_f32 v[28:29], v[44:45], v[28:29] neg_lo:[0,1] neg_hi:[0,1]
	v_xor_b32_e32 v33, 0x80000000, v22
	v_mov_b32_e32 v32, v23
	v_pk_add_f32 v[22:23], v[48:49], v[98:99]
	v_pk_add_f32 v[98:99], v[48:49], v[98:99] neg_lo:[0,1] neg_hi:[0,1]
	v_pk_add_f32 v[48:49], v[76:77], v[100:101] neg_lo:[0,1] neg_hi:[0,1]
	v_pk_add_f32 v[44:45], v[36:37], v[20:21]
	v_pk_add_f32 v[20:21], v[36:37], v[20:21] neg_lo:[0,1] neg_hi:[0,1]
	v_pk_add_f32 v[104:105], v[16:17], v[24:25]
	v_pk_add_f32 v[24:25], v[16:17], v[24:25] neg_lo:[0,1] neg_hi:[0,1]
	v_pk_add_f32 v[36:37], v[102:103], v[32:33]
	v_pk_add_f32 v[16:17], v[102:103], v[32:33] neg_lo:[0,1] neg_hi:[0,1]
	v_pk_add_f32 v[32:33], v[76:77], v[100:101]
	v_pk_mul_f32 v[76:77], v[10:11], v[48:49] op_sel:[0,1] op_sel_hi:[0,0] neg_lo:[1,1] neg_hi:[1,0]
	v_pk_fma_f32 v[76:77], v[10:11], v[48:49], v[76:77] op_sel_hi:[0,1,1]
	v_pk_add_f32 v[48:49], v[18:19], v[26:27]
	v_pk_add_f32 v[18:19], v[18:19], v[26:27] neg_lo:[0,1] neg_hi:[0,1]
	v_xor_b32_e32 v27, 0x80000000, v18
	v_mov_b32_e32 v26, v19
	v_pk_add_f32 v[18:19], v[96:97], v[40:41]
	v_pk_add_f32 v[40:41], v[96:97], v[40:41] neg_lo:[0,1] neg_hi:[0,1]
	v_pk_mul_f32 v[96:97], v[10:11], v[40:41] op_sel:[0,1] op_sel_hi:[0,0] neg_lo:[1,1] neg_hi:[1,0]
	v_pk_fma_f32 v[40:41], v[10:11], v[40:41], v[96:97] op_sel_hi:[0,1,1] neg_lo:[1,0,0] neg_hi:[1,0,0]
	v_pk_add_f32 v[96:97], v[22:23], v[48:49]
	v_pk_add_f32 v[22:23], v[22:23], v[48:49] neg_lo:[0,1] neg_hi:[0,1]
	v_pk_add_f32 v[48:49], v[32:33], v[18:19]
	v_pk_add_f32 v[18:19], v[32:33], v[18:19] neg_lo:[0,1] neg_hi:[0,1]
	v_pk_add_f32 v[102:103], v[96:97], v[48:49]
	v_xor_b32_e32 v101, 0x80000000, v18
	v_mov_b32_e32 v100, v19
	v_pk_add_f32 v[32:33], v[96:97], v[48:49] neg_lo:[0,1] neg_hi:[0,1]
	v_pk_add_f32 v[18:19], v[98:99], v[26:27]
	v_pk_add_f32 v[96:97], v[98:99], v[26:27] neg_lo:[0,1] neg_hi:[0,1]
	v_pk_add_f32 v[26:27], v[76:77], v[40:41]
	v_pk_add_f32 v[40:41], v[76:77], v[40:41] neg_lo:[0,1] neg_hi:[0,1]
	v_pk_add_f32 v[98:99], v[18:19], v[26:27]
	v_xor_b32_e32 v77, 0x80000000, v40
	v_mov_b32_e32 v76, v41
	v_pk_add_f32 v[26:27], v[18:19], v[26:27] neg_lo:[0,1] neg_hi:[0,1]
	v_pk_add_f32 v[40:41], v[96:97], v[76:77]
	v_pk_add_f32 v[18:19], v[96:97], v[76:77] neg_lo:[0,1] neg_hi:[0,1]
	v_pk_add_f32 v[76:77], v[38:39], v[92:93]
	v_pk_add_f32 v[92:93], v[38:39], v[92:93] neg_lo:[0,1] neg_hi:[0,1]
	v_pk_add_f32 v[38:39], v[42:43], v[78:79]
	v_pk_add_f32 v[42:43], v[42:43], v[78:79] neg_lo:[0,1] neg_hi:[0,1]
	v_pk_add_f32 v[48:49], v[22:23], v[100:101]
	v_pk_mul_f32 v[78:79], v[34:35], v[42:43] op_sel:[0,1] op_sel_hi:[0,0] neg_lo:[1,1] neg_hi:[1,0]
	v_pk_fma_f32 v[42:43], v[30:31], v[42:43], v[78:79] op_sel_hi:[0,1,1]
	v_pk_add_f32 v[78:79], v[46:47], v[80:81]
	v_pk_add_f32 v[46:47], v[46:47], v[80:81] neg_lo:[0,1] neg_hi:[0,1]
	v_pk_add_f32 v[22:23], v[22:23], v[100:101] neg_lo:[0,1] neg_hi:[0,1]
	v_pk_mul_f32 v[80:81], v[10:11], v[46:47] op_sel:[0,1] op_sel_hi:[0,0] neg_lo:[1,1] neg_hi:[1,0]
	v_pk_fma_f32 v[80:81], v[10:11], v[46:47], v[80:81] op_sel_hi:[0,1,1]
	v_pk_add_f32 v[46:47], v[50:51], v[82:83]
	v_pk_add_f32 v[50:51], v[50:51], v[82:83] neg_lo:[0,1] neg_hi:[0,1]
	v_pk_mul_f32 v[82:83], v[30:31], v[50:51] op_sel:[0,1] op_sel_hi:[0,0] neg_lo:[1,1] neg_hi:[1,0]
	v_pk_fma_f32 v[50:51], v[34:35], v[50:51], v[82:83] op_sel_hi:[0,1,1]
	v_pk_add_f32 v[82:83], v[52:53], v[84:85]
	v_pk_add_f32 v[52:53], v[52:53], v[84:85] neg_lo:[0,1] neg_hi:[0,1]
	v_xor_b32_e32 v85, 0x80000000, v52
	v_mov_b32_e32 v84, v53
	v_pk_add_f32 v[52:53], v[54:55], v[86:87]
	v_pk_add_f32 v[54:55], v[54:55], v[86:87] neg_lo:[0,1] neg_hi:[0,1]
	v_pk_mul_f32 v[86:87], v[30:31], v[54:55] op_sel:[0,1] op_sel_hi:[0,0] neg_lo:[1,1] neg_hi:[1,0]
	v_pk_fma_f32 v[54:55], v[34:35], v[54:55], v[86:87] op_sel_hi:[0,1,1] neg_lo:[1,0,0] neg_hi:[1,0,0]
	v_pk_add_f32 v[86:87], v[56:57], v[88:89]
	v_pk_add_f32 v[56:57], v[56:57], v[88:89] neg_lo:[0,1] neg_hi:[0,1]
	v_pk_mul_f32 v[88:89], v[10:11], v[56:57] op_sel:[0,1] op_sel_hi:[0,0] neg_lo:[1,1] neg_hi:[1,0]
	v_pk_fma_f32 v[56:57], v[10:11], v[56:57], v[88:89] op_sel_hi:[0,1,1] neg_lo:[1,0,0] neg_hi:[1,0,0]
	v_pk_add_f32 v[88:89], v[58:59], v[90:91]
	v_pk_add_f32 v[58:59], v[58:59], v[90:91] neg_lo:[0,1] neg_hi:[0,1]
	v_pk_mul_f32 v[34:35], v[34:35], v[58:59] op_sel:[0,1] op_sel_hi:[0,0] neg_lo:[1,1] neg_hi:[1,0]
	v_pk_fma_f32 v[34:35], v[30:31], v[58:59], v[34:35] op_sel_hi:[0,1,1] neg_lo:[1,0,0] neg_hi:[1,0,0]
	v_pk_add_f32 v[30:31], v[76:77], v[82:83]
	v_pk_add_f32 v[58:59], v[76:77], v[82:83] neg_lo:[0,1] neg_hi:[0,1]
	v_pk_add_f32 v[76:77], v[52:53], v[38:39]
	v_pk_add_f32 v[38:39], v[38:39], v[52:53] neg_lo:[0,1] neg_hi:[0,1]
	v_pk_mul_f32 v[52:53], v[10:11], v[38:39] op_sel:[0,1] op_sel_hi:[0,0] neg_lo:[1,1] neg_hi:[1,0]
	v_pk_fma_f32 v[52:53], v[10:11], v[38:39], v[52:53] op_sel_hi:[0,1,1]
	v_pk_add_f32 v[38:39], v[78:79], v[86:87]
	v_pk_add_f32 v[78:79], v[78:79], v[86:87] neg_lo:[0,1] neg_hi:[0,1]
	v_xor_b32_e32 v83, 0x80000000, v78
	v_mov_b32_e32 v82, v79
	v_pk_add_f32 v[78:79], v[46:47], v[88:89]
	v_pk_add_f32 v[46:47], v[46:47], v[88:89] neg_lo:[0,1] neg_hi:[0,1]
	v_pk_add_f32 v[88:89], v[76:77], v[78:79]
	v_pk_mul_f32 v[86:87], v[10:11], v[46:47] op_sel:[0,1] op_sel_hi:[0,0] neg_lo:[1,1] neg_hi:[1,0]
	v_pk_fma_f32 v[46:47], v[10:11], v[46:47], v[86:87] op_sel_hi:[0,1,1] neg_lo:[1,0,0] neg_hi:[1,0,0]
	v_pk_add_f32 v[86:87], v[30:31], v[38:39]
	v_pk_add_f32 v[30:31], v[30:31], v[38:39] neg_lo:[0,1] neg_hi:[0,1]
	v_pk_add_f32 v[38:39], v[76:77], v[78:79] neg_lo:[0,1] neg_hi:[0,1]
	v_pk_add_f32 v[78:79], v[86:87], v[88:89] neg_lo:[0,1] neg_hi:[0,1]
	v_pk_add_f32 v[90:91], v[30:31], v[38:39] op_sel:[0,1] op_sel_hi:[1,0] neg_hi:[0,1]
	v_pk_add_f32 v[38:39], v[30:31], v[38:39] op_sel:[0,1] op_sel_hi:[1,0] neg_lo:[0,1]
	v_pk_add_f32 v[76:77], v[52:53], v[46:47]
	v_pk_add_f32 v[46:47], v[52:53], v[46:47] neg_lo:[0,1] neg_hi:[0,1]
	v_pk_add_f32 v[30:31], v[58:59], v[82:83]
	v_pk_add_f32 v[58:59], v[58:59], v[82:83] neg_lo:[0,1] neg_hi:[0,1]
	v_xor_b32_e32 v53, 0x80000000, v46
	v_mov_b32_e32 v52, v47
	v_pk_add_f32 v[82:83], v[30:31], v[76:77]
	v_pk_add_f32 v[46:47], v[30:31], v[76:77] neg_lo:[0,1] neg_hi:[0,1]
	v_pk_add_f32 v[76:77], v[58:59], v[52:53]
	v_pk_add_f32 v[30:31], v[58:59], v[52:53] neg_lo:[0,1] neg_hi:[0,1]
	v_pk_add_f32 v[52:53], v[92:93], v[84:85]
	v_pk_add_f32 v[58:59], v[92:93], v[84:85] neg_lo:[0,1] neg_hi:[0,1]
	v_pk_add_f32 v[84:85], v[54:55], v[42:43]
	v_pk_add_f32 v[42:43], v[42:43], v[54:55] neg_lo:[0,1] neg_hi:[0,1]
	v_pk_add_f32 v[86:87], v[86:87], v[88:89]
	v_pk_mul_f32 v[54:55], v[10:11], v[42:43] op_sel:[0,1] op_sel_hi:[0,0] neg_lo:[1,1] neg_hi:[1,0]
	v_pk_fma_f32 v[54:55], v[10:11], v[42:43], v[54:55] op_sel_hi:[0,1,1]
	v_pk_add_f32 v[42:43], v[80:81], v[56:57]
	v_pk_add_f32 v[56:57], v[80:81], v[56:57] neg_lo:[0,1] neg_hi:[0,1]
	v_xor_b32_e32 v81, 0x80000000, v56
	v_mov_b32_e32 v80, v57
	v_pk_add_f32 v[56:57], v[50:51], v[34:35]
	v_pk_add_f32 v[34:35], v[50:51], v[34:35] neg_lo:[0,1] neg_hi:[0,1]
	v_pk_mul_f32 v[50:51], v[10:11], v[34:35] op_sel:[0,1] op_sel_hi:[0,0] neg_lo:[1,1] neg_hi:[1,0]
	v_pk_fma_f32 v[34:35], v[10:11], v[34:35], v[50:51] op_sel_hi:[0,1,1] neg_lo:[1,0,0] neg_hi:[1,0,0]
	v_pk_add_f32 v[50:51], v[52:53], v[42:43]
	v_pk_add_f32 v[42:43], v[52:53], v[42:43] neg_lo:[0,1] neg_hi:[0,1]
	v_pk_add_f32 v[52:53], v[84:85], v[56:57]
	v_pk_add_f32 v[56:57], v[84:85], v[56:57] neg_lo:[0,1] neg_hi:[0,1]
	v_xor_b32_e32 v85, 0x80000000, v56
	v_mov_b32_e32 v84, v57
	v_pk_add_f32 v[56:57], v[50:51], v[52:53]
	v_pk_add_f32 v[50:51], v[50:51], v[52:53] neg_lo:[0,1] neg_hi:[0,1]
	v_pk_add_f32 v[52:53], v[42:43], v[84:85]
	v_pk_add_f32 v[42:43], v[42:43], v[84:85] neg_lo:[0,1] neg_hi:[0,1]
	v_pk_add_f32 v[84:85], v[58:59], v[80:81]
	v_pk_add_f32 v[58:59], v[58:59], v[80:81] neg_lo:[0,1] neg_hi:[0,1]
	v_pk_add_f32 v[80:81], v[54:55], v[34:35]
	v_pk_add_f32 v[34:35], v[54:55], v[34:35] neg_lo:[0,1] neg_hi:[0,1]
	v_pk_add_f32 v[92:93], v[84:85], v[80:81]
	v_pk_add_f32 v[80:81], v[84:85], v[80:81] neg_lo:[0,1] neg_hi:[0,1]
	v_pk_add_f32 v[84:85], v[58:59], v[34:35] op_sel:[0,1] op_sel_hi:[1,0] neg_hi:[0,1]
	v_pk_add_f32 v[34:35], v[58:59], v[34:35] op_sel:[0,1] op_sel_hi:[1,0] neg_lo:[0,1]
	v_pk_fma_f32 v[58:59], v[14:15], s[90:91], v[14:15] op_sel:[1,0,0] op_sel_hi:[0,1,1]
	v_pk_mul_f32 v[54:55], v[94:95], s[14:15] op_sel:[1,0] neg_lo:[1,0]
	v_pk_mul_f32 v[88:89], v[58:59], v[86:87] op_sel:[1,1] op_sel_hi:[0,1] neg_lo:[0,1]
	v_pk_fma_f32 v[54:55], v[94:95], s[94:95], v[54:55] op_sel_hi:[0,1,1]
	v_pk_fma_f32 v[86:87], v[58:59], v[86:87], v[88:89] op_sel_hi:[1,0,1]
	ds_write2_b64 v74, v[54:55], v[86:87] offset1:16
	v_pk_mul_f32 v[54:55], v[14:15], v[58:59] op_sel:[1,1] op_sel_hi:[0,1] neg_lo:[0,1]
	v_pk_fma_f32 v[54:55], v[14:15], v[58:59], v[54:55] op_sel_hi:[1,0,1]
	v_pk_mul_f32 v[58:59], v[54:55], v[102:103] op_sel:[1,1] op_sel_hi:[0,1] neg_lo:[0,1]
	v_pk_mul_f32 v[74:75], v[14:15], v[54:55] op_sel:[1,1] op_sel_hi:[0,1] neg_lo:[0,1]
	v_pk_fma_f32 v[58:59], v[54:55], v[102:103], v[58:59] op_sel_hi:[1,0,1]
	v_pk_fma_f32 v[54:55], v[14:15], v[54:55], v[74:75] op_sel_hi:[1,0,1]
	v_pk_mul_f32 v[74:75], v[54:55], v[56:57] op_sel:[1,1] op_sel_hi:[0,1] neg_lo:[0,1]
	v_pk_fma_f32 v[56:57], v[54:55], v[56:57], v[74:75] op_sel_hi:[1,0,1]
	ds_write2_b64 v73, v[58:59], v[56:57] offset0:32 offset1:48
	v_pk_mul_f32 v[56:57], v[14:15], v[54:55] op_sel:[1,1] op_sel_hi:[0,1] neg_lo:[0,1]
	v_pk_fma_f32 v[54:55], v[14:15], v[54:55], v[56:57] op_sel_hi:[1,0,1]
	v_pk_mul_f32 v[56:57], v[54:55], v[104:105] op_sel:[1,1] op_sel_hi:[0,1] neg_lo:[0,1]
	v_pk_mul_f32 v[58:59], v[14:15], v[54:55] op_sel:[1,1] op_sel_hi:[0,1] neg_lo:[0,1]
	v_pk_fma_f32 v[56:57], v[54:55], v[104:105], v[56:57] op_sel_hi:[1,0,1]
	v_pk_fma_f32 v[54:55], v[14:15], v[54:55], v[58:59] op_sel_hi:[1,0,1]
	v_pk_mul_f32 v[58:59], v[54:55], v[82:83] op_sel:[1,1] op_sel_hi:[0,1] neg_lo:[0,1]
	v_pk_fma_f32 v[58:59], v[54:55], v[82:83], v[58:59] op_sel_hi:[1,0,1]
	ds_write2_b64 v72, v[56:57], v[58:59] offset0:64 offset1:80
	v_pk_mul_f32 v[56:57], v[14:15], v[54:55] op_sel:[1,1] op_sel_hi:[0,1] neg_lo:[0,1]
	v_pk_fma_f32 v[54:55], v[14:15], v[54:55], v[56:57] op_sel_hi:[1,0,1]
	v_pk_mul_f32 v[56:57], v[54:55], v[98:99] op_sel:[1,1] op_sel_hi:[0,1] neg_lo:[0,1]
	v_pk_mul_f32 v[58:59], v[14:15], v[54:55] op_sel:[1,1] op_sel_hi:[0,1] neg_lo:[0,1]
	v_pk_fma_f32 v[56:57], v[54:55], v[98:99], v[56:57] op_sel_hi:[1,0,1]
	v_pk_fma_f32 v[54:55], v[14:15], v[54:55], v[58:59] op_sel_hi:[1,0,1]
	v_pk_mul_f32 v[58:59], v[54:55], v[92:93] op_sel:[1,1] op_sel_hi:[0,1] neg_lo:[0,1]
	v_pk_fma_f32 v[58:59], v[54:55], v[92:93], v[58:59] op_sel_hi:[1,0,1]
	ds_write2_b64 v71, v[56:57], v[58:59] offset0:96 offset1:112
	v_pk_mul_f32 v[56:57], v[14:15], v[54:55] op_sel:[1,1] op_sel_hi:[0,1] neg_lo:[0,1]
	v_pk_fma_f32 v[54:55], v[14:15], v[54:55], v[56:57] op_sel_hi:[1,0,1]
	v_pk_mul_f32 v[56:57], v[54:55], v[44:45] op_sel:[1,1] op_sel_hi:[0,1] neg_lo:[0,1]
	v_pk_fma_f32 v[44:45], v[54:55], v[44:45], v[56:57] op_sel_hi:[1,0,1]
	v_pk_mul_f32 v[56:57], v[14:15], v[54:55] op_sel:[1,1] op_sel_hi:[0,1] neg_lo:[0,1]
	v_pk_fma_f32 v[54:55], v[14:15], v[54:55], v[56:57] op_sel_hi:[1,0,1]
	v_pk_mul_f32 v[56:57], v[54:55], v[90:91] op_sel:[1,1] op_sel_hi:[0,1] neg_lo:[0,1]
	v_pk_fma_f32 v[56:57], v[54:55], v[90:91], v[56:57] op_sel_hi:[1,0,1]
	ds_write2_b64 v70, v[44:45], v[56:57] offset0:128 offset1:144
	v_pk_mul_f32 v[44:45], v[14:15], v[54:55] op_sel:[1,1] op_sel_hi:[0,1] neg_lo:[0,1]
	v_pk_fma_f32 v[44:45], v[14:15], v[54:55], v[44:45] op_sel_hi:[1,0,1]
	v_pk_mul_f32 v[54:55], v[44:45], v[48:49] op_sel:[1,1] op_sel_hi:[0,1] neg_lo:[0,1]
	v_pk_fma_f32 v[48:49], v[44:45], v[48:49], v[54:55] op_sel_hi:[1,0,1]
	v_pk_mul_f32 v[54:55], v[14:15], v[44:45] op_sel:[1,1] op_sel_hi:[0,1] neg_lo:[0,1]
	v_pk_fma_f32 v[44:45], v[14:15], v[44:45], v[54:55] op_sel_hi:[1,0,1]
	v_pk_mul_f32 v[54:55], v[44:45], v[52:53] op_sel:[1,1] op_sel_hi:[0,1] neg_lo:[0,1]
	v_pk_fma_f32 v[52:53], v[44:45], v[52:53], v[54:55] op_sel_hi:[1,0,1]
	ds_write2_b64 v69, v[48:49], v[52:53] offset0:160 offset1:176
	v_pk_mul_f32 v[48:49], v[14:15], v[44:45] op_sel:[1,1] op_sel_hi:[0,1] neg_lo:[0,1]
	v_pk_fma_f32 v[44:45], v[14:15], v[44:45], v[48:49] op_sel_hi:[1,0,1]
	v_pk_mul_f32 v[48:49], v[36:37], v[44:45] op_sel:[1,1] op_sel_hi:[1,0] neg_lo:[1,0]
	v_pk_fma_f32 v[36:37], v[36:37], v[44:45], v[48:49] op_sel_hi:[0,1,1]
	v_pk_mul_f32 v[48:49], v[14:15], v[44:45] op_sel:[1,1] op_sel_hi:[0,1] neg_lo:[0,1]
	v_pk_fma_f32 v[44:45], v[14:15], v[44:45], v[48:49] op_sel_hi:[1,0,1]
	v_pk_mul_f32 v[48:49], v[44:45], v[76:77] op_sel:[1,1] op_sel_hi:[0,1] neg_lo:[0,1]
	v_pk_fma_f32 v[48:49], v[44:45], v[76:77], v[48:49] op_sel_hi:[1,0,1]
	ds_write2_b64 v68, v[36:37], v[48:49] offset0:192 offset1:208
	v_pk_mul_f32 v[36:37], v[14:15], v[44:45] op_sel:[1,1] op_sel_hi:[0,1] neg_lo:[0,1]
	v_pk_fma_f32 v[36:37], v[14:15], v[44:45], v[36:37] op_sel_hi:[1,0,1]
	v_pk_mul_f32 v[44:45], v[40:41], v[36:37] op_sel:[1,1] op_sel_hi:[1,0] neg_lo:[1,0]
	v_pk_fma_f32 v[40:41], v[40:41], v[36:37], v[44:45] op_sel_hi:[0,1,1]
	v_pk_mul_f32 v[44:45], v[14:15], v[36:37] op_sel:[1,1] op_sel_hi:[0,1] neg_lo:[0,1]
	v_pk_fma_f32 v[36:37], v[14:15], v[36:37], v[44:45] op_sel_hi:[1,0,1]
	v_pk_mul_f32 v[44:45], v[36:37], v[84:85] op_sel:[1,1] op_sel_hi:[0,1] neg_lo:[0,1]
	v_pk_fma_f32 v[44:45], v[36:37], v[84:85], v[44:45] op_sel_hi:[1,0,1]
	ds_write2_b64 v67, v[40:41], v[44:45] offset0:224 offset1:240
	v_pk_mul_f32 v[40:41], v[14:15], v[36:37] op_sel:[1,1] op_sel_hi:[0,1] neg_lo:[0,1]
	v_pk_fma_f32 v[36:37], v[14:15], v[36:37], v[40:41] op_sel_hi:[1,0,1]
	v_pk_mul_f32 v[40:41], v[28:29], v[36:37] op_sel:[1,1] op_sel_hi:[1,0] neg_lo:[1,0]
	v_pk_fma_f32 v[28:29], v[28:29], v[36:37], v[40:41] op_sel_hi:[0,1,1]
	v_pk_mul_f32 v[40:41], v[14:15], v[36:37] op_sel:[1,1] op_sel_hi:[0,1] neg_lo:[0,1]
	v_pk_fma_f32 v[36:37], v[14:15], v[36:37], v[40:41] op_sel_hi:[1,0,1]
	v_pk_mul_f32 v[40:41], v[78:79], v[36:37] op_sel:[1,1] op_sel_hi:[1,0] neg_lo:[1,0]
	v_pk_fma_f32 v[40:41], v[78:79], v[36:37], v[40:41] op_sel_hi:[0,1,1]
	ds_write2_b64 v66, v[28:29], v[40:41] offset1:16
	v_pk_mul_f32 v[28:29], v[14:15], v[36:37] op_sel:[1,1] op_sel_hi:[0,1] neg_lo:[0,1]
	v_pk_fma_f32 v[28:29], v[14:15], v[36:37], v[28:29] op_sel_hi:[1,0,1]
	v_pk_mul_f32 v[36:37], v[32:33], v[28:29] op_sel:[1,1] op_sel_hi:[1,0] neg_lo:[1,0]
	v_pk_fma_f32 v[32:33], v[32:33], v[28:29], v[36:37] op_sel_hi:[0,1,1]
	v_pk_mul_f32 v[36:37], v[14:15], v[28:29] op_sel:[1,1] op_sel_hi:[0,1] neg_lo:[0,1]
	v_pk_fma_f32 v[28:29], v[14:15], v[28:29], v[36:37] op_sel_hi:[1,0,1]
	v_pk_mul_f32 v[36:37], v[50:51], v[28:29] op_sel:[1,1] op_sel_hi:[1,0] neg_lo:[1,0]
	v_pk_fma_f32 v[36:37], v[50:51], v[28:29], v[36:37] op_sel_hi:[0,1,1]
	ds_write2_b64 v65, v[32:33], v[36:37] offset0:32 offset1:48
	v_pk_mul_f32 v[32:33], v[14:15], v[28:29] op_sel:[1,1] op_sel_hi:[0,1] neg_lo:[0,1]
	v_pk_fma_f32 v[28:29], v[14:15], v[28:29], v[32:33] op_sel_hi:[1,0,1]
	v_pk_mul_f32 v[32:33], v[24:25], v[28:29] op_sel:[1,1] op_sel_hi:[1,0] neg_lo:[1,0]
	v_pk_fma_f32 v[24:25], v[24:25], v[28:29], v[32:33] op_sel_hi:[0,1,1]
	v_pk_mul_f32 v[32:33], v[14:15], v[28:29] op_sel:[1,1] op_sel_hi:[0,1] neg_lo:[0,1]
	v_pk_fma_f32 v[28:29], v[14:15], v[28:29], v[32:33] op_sel_hi:[1,0,1]
	v_pk_mul_f32 v[32:33], v[46:47], v[28:29] op_sel:[1,1] op_sel_hi:[1,0] neg_lo:[1,0]
	v_pk_fma_f32 v[32:33], v[46:47], v[28:29], v[32:33] op_sel_hi:[0,1,1]
	ds_write2_b64 v64, v[24:25], v[32:33] offset0:64 offset1:80
	v_pk_mul_f32 v[24:25], v[14:15], v[28:29] op_sel:[1,1] op_sel_hi:[0,1] neg_lo:[0,1]
	v_pk_fma_f32 v[24:25], v[14:15], v[28:29], v[24:25] op_sel_hi:[1,0,1]
	v_pk_mul_f32 v[28:29], v[26:27], v[24:25] op_sel:[1,1] op_sel_hi:[1,0] neg_lo:[1,0]
	v_pk_fma_f32 v[26:27], v[26:27], v[24:25], v[28:29] op_sel_hi:[0,1,1]
	v_pk_mul_f32 v[28:29], v[14:15], v[24:25] op_sel:[1,1] op_sel_hi:[0,1] neg_lo:[0,1]
	v_pk_fma_f32 v[24:25], v[14:15], v[24:25], v[28:29] op_sel_hi:[1,0,1]
	v_pk_mul_f32 v[28:29], v[80:81], v[24:25] op_sel:[1,1] op_sel_hi:[1,0] neg_lo:[1,0]
	v_pk_fma_f32 v[28:29], v[80:81], v[24:25], v[28:29] op_sel_hi:[0,1,1]
	ds_write2_b64 v63, v[26:27], v[28:29] offset0:96 offset1:112
	v_pk_mul_f32 v[26:27], v[14:15], v[24:25] op_sel:[1,1] op_sel_hi:[0,1] neg_lo:[0,1]
	v_pk_fma_f32 v[24:25], v[14:15], v[24:25], v[26:27] op_sel_hi:[1,0,1]
	v_pk_mul_f32 v[26:27], v[20:21], v[24:25] op_sel:[1,1] op_sel_hi:[1,0] neg_lo:[1,0]
	v_pk_fma_f32 v[20:21], v[20:21], v[24:25], v[26:27] op_sel_hi:[0,1,1]
	v_pk_mul_f32 v[26:27], v[14:15], v[24:25] op_sel:[1,1] op_sel_hi:[0,1] neg_lo:[0,1]
	v_pk_fma_f32 v[24:25], v[14:15], v[24:25], v[26:27] op_sel_hi:[1,0,1]
	v_pk_mul_f32 v[26:27], v[38:39], v[24:25] op_sel:[1,1] op_sel_hi:[1,0] neg_lo:[1,0]
	v_pk_fma_f32 v[26:27], v[38:39], v[24:25], v[26:27] op_sel_hi:[0,1,1]
	ds_write2_b64 v62, v[20:21], v[26:27] offset0:128 offset1:144
	v_pk_mul_f32 v[20:21], v[14:15], v[24:25] op_sel:[1,1] op_sel_hi:[0,1] neg_lo:[0,1]
	v_pk_fma_f32 v[20:21], v[14:15], v[24:25], v[20:21] op_sel_hi:[1,0,1]
	v_pk_mul_f32 v[24:25], v[22:23], v[20:21] op_sel:[1,1] op_sel_hi:[1,0] neg_lo:[1,0]
	v_pk_fma_f32 v[22:23], v[22:23], v[20:21], v[24:25] op_sel_hi:[0,1,1]
	v_pk_mul_f32 v[24:25], v[14:15], v[20:21] op_sel:[1,1] op_sel_hi:[0,1] neg_lo:[0,1]
	v_pk_fma_f32 v[20:21], v[14:15], v[20:21], v[24:25] op_sel_hi:[1,0,1]
	v_pk_mul_f32 v[24:25], v[42:43], v[20:21] op_sel:[1,1] op_sel_hi:[1,0] neg_lo:[1,0]
	v_pk_fma_f32 v[24:25], v[42:43], v[20:21], v[24:25] op_sel_hi:[0,1,1]
	ds_write2_b64 v61, v[22:23], v[24:25] offset0:160 offset1:176
	v_pk_mul_f32 v[22:23], v[14:15], v[20:21] op_sel:[1,1] op_sel_hi:[0,1] neg_lo:[0,1]
	v_pk_fma_f32 v[20:21], v[14:15], v[20:21], v[22:23] op_sel_hi:[1,0,1]
	v_pk_mul_f32 v[22:23], v[16:17], v[20:21] op_sel:[1,1] op_sel_hi:[1,0] neg_lo:[1,0]
	v_pk_fma_f32 v[16:17], v[16:17], v[20:21], v[22:23] op_sel_hi:[0,1,1]
	v_pk_mul_f32 v[22:23], v[14:15], v[20:21] op_sel:[1,1] op_sel_hi:[0,1] neg_lo:[0,1]
	v_pk_fma_f32 v[20:21], v[14:15], v[20:21], v[22:23] op_sel_hi:[1,0,1]
	v_pk_mul_f32 v[22:23], v[30:31], v[20:21] op_sel:[1,1] op_sel_hi:[1,0] neg_lo:[1,0]
	v_pk_fma_f32 v[22:23], v[30:31], v[20:21], v[22:23] op_sel_hi:[0,1,1]
	ds_write2_b64 v60, v[16:17], v[22:23] offset0:192 offset1:208
	v_pk_mul_f32 v[16:17], v[14:15], v[20:21] op_sel:[1,1] op_sel_hi:[0,1] neg_lo:[0,1]
	v_pk_fma_f32 v[16:17], v[14:15], v[20:21], v[16:17] op_sel_hi:[1,0,1]
	v_pk_mul_f32 v[20:21], v[18:19], v[16:17] op_sel:[1,1] op_sel_hi:[1,0] neg_lo:[1,0]
	v_pk_fma_f32 v[18:19], v[18:19], v[16:17], v[20:21] op_sel_hi:[0,1,1]
	v_pk_mul_f32 v[20:21], v[14:15], v[16:17] op_sel:[1,1] op_sel_hi:[0,1] neg_lo:[0,1]
	v_pk_fma_f32 v[14:15], v[14:15], v[16:17], v[20:21] op_sel_hi:[1,0,1]
	v_pk_mul_f32 v[16:17], v[34:35], v[14:15] op_sel:[1,1] op_sel_hi:[1,0] neg_lo:[1,0]
	v_pk_fma_f32 v[14:15], v[34:35], v[14:15], v[16:17] op_sel_hi:[0,1,1]
	ds_write2_b64 v13, v[18:19], v[14:15] offset0:224 offset1:240
	v_mov_b32_e32 v14, v182
	v_mov_b32_e32 v10, v176
	v_mov_b32_e32 v13, v175
	s_waitcnt lgkmcnt(0)
	s_barrier
	v_mov_b32_e32 v48, v167
	v_xor_b32_e32 v16, 1, v13
	v_lshlrev_b32_e32 v10, 3, v10
	v_lshlrev_b32_e32 v16, 3, v16
	v_add3_u32 v18, 0, v16, v10
	v_xor_b32_e32 v16, 2, v13
	v_lshlrev_b32_e32 v16, 3, v16
	v_xor_b32_e32 v24, 5, v13
	v_add3_u32 v20, 0, v16, v10
	v_xor_b32_e32 v16, 3, v13
	v_lshlrev_b32_e32 v24, 3, v24
	v_lshlrev_b32_e32 v15, 3, v13
	v_lshlrev_b32_e32 v16, 3, v16
	v_add3_u32 v26, 0, v24, v10
	v_xor_b32_e32 v24, 6, v13
	v_add3_u32 v15, 0, v15, v10
	v_add3_u32 v22, 0, v16, v10
	v_lshlrev_b32_e32 v24, 3, v24
	v_xor_b32_e32 v32, 9, v13
	ds_read_b64 v[16:17], v15
	ds_read_b64 v[18:19], v18
	ds_read_b64 v[20:21], v20
	ds_read_b64 v[22:23], v22
	v_xor_b32_e32 v15, 4, v13
	v_add3_u32 v28, 0, v24, v10
	v_xor_b32_e32 v24, 7, v13
	v_lshlrev_b32_e32 v32, 3, v32
	v_lshlrev_b32_e32 v15, 3, v15
	v_lshlrev_b32_e32 v24, 3, v24
	v_add3_u32 v34, 0, v32, v10
	v_xor_b32_e32 v32, 10, v13
	v_add3_u32 v15, 0, v15, v10
	v_add3_u32 v30, 0, v24, v10
	v_lshlrev_b32_e32 v32, 3, v32
	ds_read_b64 v[24:25], v15
	ds_read_b64 v[26:27], v26
	ds_read_b64 v[28:29], v28
	ds_read_b64 v[30:31], v30
	v_xor_b32_e32 v15, 8, v13
	v_add3_u32 v36, 0, v32, v10
	v_xor_b32_e32 v32, 11, v13
	v_lshlrev_b32_e32 v15, 3, v15
	v_lshlrev_b32_e32 v32, 3, v32
	v_xor_b32_e32 v40, 13, v13
	v_add3_u32 v15, 0, v15, v10
	v_add3_u32 v38, 0, v32, v10
	v_lshlrev_b32_e32 v40, 3, v40
	ds_read_b64 v[32:33], v15
	ds_read_b64 v[34:35], v34
	ds_read_b64 v[36:37], v36
	ds_read_b64 v[38:39], v38
	v_xor_b32_e32 v15, 12, v13
	v_add3_u32 v42, 0, v40, v10
	v_xor_b32_e32 v40, 14, v13
	v_xor_b32_e32 v13, 15, v13
	v_lshlrev_b32_e32 v15, 3, v15
	v_lshlrev_b32_e32 v40, 3, v40
	v_lshlrev_b32_e32 v13, 3, v13
	v_add3_u32 v15, 0, v15, v10
	v_add3_u32 v44, 0, v40, v10
	v_add3_u32 v10, 0, v13, v10
	ds_read_b64 v[40:41], v15
	ds_read_b64 v[42:43], v42
	ds_read_b64 v[44:45], v44
	ds_read_b64 v[46:47], v10
	v_mov_b32_e32 v10, v1
	v_mov_b32_e32 v13, v166
	v_mov_b32_e32 v10, v164
	s_waitcnt lgkmcnt(7)
	v_pk_add_f32 v[52:53], v[16:17], v[32:33]
	v_mov_b32_e32 v10, v165
	v_pk_add_f32 v[16:17], v[16:17], v[32:33] neg_lo:[0,1] neg_hi:[0,1]
	s_waitcnt lgkmcnt(6)
	v_pk_add_f32 v[32:33], v[18:19], v[34:35]
	v_pk_add_f32 v[18:19], v[18:19], v[34:35] neg_lo:[0,1] neg_hi:[0,1]
	v_mov_b32_e32 v13, v168
	v_mov_b32_e32 v50, v169
	v_ashrrev_i32_e32 v15, 31, v14
	v_pk_mul_f32 v[34:35], v[18:19], v[50:51] op_sel:[1,0] op_sel_hi:[0,0] neg_lo:[1,1] neg_hi:[0,1]
	v_mov_b32_e32 v13, v170
	v_pk_fma_f32 v[18:19], v[18:19], v[10:11], v[34:35] op_sel_hi:[1,0,1]
	s_waitcnt lgkmcnt(5)
	v_pk_add_f32 v[34:35], v[20:21], v[36:37]
	v_pk_add_f32 v[20:21], v[20:21], v[36:37] neg_lo:[0,1] neg_hi:[0,1]
	v_pk_mul_f32 v[36:37], v[20:21], v[48:49] op_sel:[1,0] op_sel_hi:[0,0] neg_lo:[1,1] neg_hi:[0,1]
	v_mov_b32_e32 v13, v171
	v_pk_fma_f32 v[20:21], v[20:21], v[48:49], v[36:37] op_sel_hi:[1,0,1]
	s_waitcnt lgkmcnt(4)
	v_pk_add_f32 v[36:37], v[22:23], v[38:39]
	v_pk_add_f32 v[22:23], v[22:23], v[38:39] neg_lo:[0,1] neg_hi:[0,1]
	v_pk_mul_f32 v[38:39], v[22:23], v[50:51] op_sel_hi:[1,0]
	v_pk_fma_f32 v[22:23], v[22:23], v[10:11], v[38:39] op_sel:[1,0,0] op_sel_hi:[0,0,1] neg_lo:[1,1,0] neg_hi:[0,1,0]
	s_waitcnt lgkmcnt(3)
	v_pk_add_f32 v[38:39], v[24:25], v[40:41]
	v_pk_add_f32 v[24:25], v[24:25], v[40:41] neg_lo:[0,1] neg_hi:[0,1]
	v_mov_b32_e32 v13, v175
	v_xor_b32_e32 v41, 0x80000000, v24
	v_mov_b32_e32 v40, v25
	s_waitcnt lgkmcnt(2)
	v_pk_add_f32 v[24:25], v[26:27], v[42:43]
	v_pk_add_f32 v[26:27], v[26:27], v[42:43] neg_lo:[0,1] neg_hi:[0,1]
	v_pk_mul_f32 v[42:43], v[26:27], v[50:51] op_sel_hi:[1,0] neg_lo:[0,1] neg_hi:[0,1]
	v_pk_fma_f32 v[26:27], v[26:27], v[10:11], v[42:43] op_sel:[1,0,0] op_sel_hi:[0,0,1] neg_lo:[1,1,0] neg_hi:[0,1,0]
	s_waitcnt lgkmcnt(1)
	v_pk_add_f32 v[42:43], v[28:29], v[44:45]
	v_pk_add_f32 v[28:29], v[28:29], v[44:45] neg_lo:[0,1] neg_hi:[0,1]
	v_pk_mul_f32 v[44:45], v[28:29], v[48:49] op_sel:[1,0] op_sel_hi:[0,0] neg_lo:[1,1] neg_hi:[0,1]
	v_pk_fma_f32 v[28:29], v[28:29], v[48:49], v[44:45] op_sel_hi:[1,0,1] neg_lo:[0,1,0] neg_hi:[0,1,0]
	s_waitcnt lgkmcnt(0)
	v_pk_add_f32 v[44:45], v[30:31], v[46:47]
	v_pk_add_f32 v[30:31], v[30:31], v[46:47] neg_lo:[0,1] neg_hi:[0,1]
	v_pk_mul_f32 v[46:47], v[30:31], v[50:51] op_sel:[1,0] op_sel_hi:[0,0] neg_lo:[1,1] neg_hi:[0,1]
	v_pk_add_f32 v[50:51], v[32:33], v[24:25]
	v_pk_add_f32 v[24:25], v[32:33], v[24:25] neg_lo:[0,1] neg_hi:[0,1]
	v_pk_fma_f32 v[30:31], v[30:31], v[10:11], v[46:47] op_sel_hi:[1,0,1] neg_lo:[0,1,0] neg_hi:[0,1,0]
	v_pk_mul_f32 v[32:33], v[24:25], v[48:49] op_sel:[1,0] op_sel_hi:[0,0] neg_lo:[1,1] neg_hi:[0,1]
	v_pk_add_f32 v[46:47], v[52:53], v[38:39]
	v_pk_fma_f32 v[24:25], v[24:25], v[48:49], v[32:33] op_sel_hi:[1,0,1]
	v_pk_add_f32 v[32:33], v[34:35], v[42:43]
	v_pk_add_f32 v[34:35], v[34:35], v[42:43] neg_lo:[0,1] neg_hi:[0,1]
	v_pk_add_f32 v[38:39], v[52:53], v[38:39] neg_lo:[0,1] neg_hi:[0,1]
	v_xor_b32_e32 v43, 0x80000000, v34
	v_mov_b32_e32 v42, v35
	v_pk_add_f32 v[34:35], v[36:37], v[44:45]
	v_pk_add_f32 v[36:37], v[36:37], v[44:45] neg_lo:[0,1] neg_hi:[0,1]
	v_mov_b32_e32 v10, v177
	v_pk_mul_f32 v[44:45], v[36:37], v[48:49] op_sel:[1,0] op_sel_hi:[0,0] neg_lo:[1,1] neg_hi:[0,1]
	v_pk_fma_f32 v[36:37], v[36:37], v[48:49], v[44:45] op_sel_hi:[1,0,1] neg_lo:[0,1,0] neg_hi:[0,1,0]
	v_pk_add_f32 v[44:45], v[46:47], v[32:33]
	v_pk_add_f32 v[32:33], v[46:47], v[32:33] neg_lo:[0,1] neg_hi:[0,1]
	v_pk_add_f32 v[46:47], v[50:51], v[34:35]
	v_pk_add_f32 v[34:35], v[50:51], v[34:35] neg_lo:[0,1] neg_hi:[0,1]
	v_xor_b32_e32 v51, 0x80000000, v34
	v_mov_b32_e32 v50, v35
	v_pk_add_f32 v[34:35], v[44:45], v[46:47]
	v_pk_add_f32 v[44:45], v[44:45], v[46:47] neg_lo:[0,1] neg_hi:[0,1]
	v_pk_add_f32 v[46:47], v[32:33], v[50:51]
	v_pk_add_f32 v[32:33], v[32:33], v[50:51] neg_lo:[0,1] neg_hi:[0,1]
	v_pk_add_f32 v[50:51], v[38:39], v[42:43]
	v_pk_add_f32 v[38:39], v[38:39], v[42:43] neg_lo:[0,1] neg_hi:[0,1]
	v_pk_add_f32 v[42:43], v[24:25], v[36:37]
	v_pk_add_f32 v[24:25], v[24:25], v[36:37] neg_lo:[0,1] neg_hi:[0,1]
	v_xor_b32_e32 v37, 0x80000000, v24
	v_mov_b32_e32 v36, v25
	v_pk_add_f32 v[24:25], v[50:51], v[42:43]
	v_pk_add_f32 v[42:43], v[50:51], v[42:43] neg_lo:[0,1] neg_hi:[0,1]
	v_pk_add_f32 v[50:51], v[38:39], v[36:37]
	v_pk_add_f32 v[36:37], v[38:39], v[36:37] neg_lo:[0,1] neg_hi:[0,1]
	v_pk_add_f32 v[38:39], v[16:17], v[40:41]
	v_pk_add_f32 v[16:17], v[16:17], v[40:41] neg_lo:[0,1] neg_hi:[0,1]
	v_pk_add_f32 v[40:41], v[18:19], v[26:27]
	v_pk_add_f32 v[18:19], v[18:19], v[26:27] neg_lo:[0,1] neg_hi:[0,1]
	v_pk_mul_f32 v[26:27], v[48:49], v[18:19] op_sel:[0,1] op_sel_hi:[0,0] neg_lo:[1,1] neg_hi:[1,0]
	v_pk_fma_f32 v[18:19], v[48:49], v[18:19], v[26:27] op_sel_hi:[0,1,1]
	v_pk_add_f32 v[26:27], v[20:21], v[28:29]
	v_pk_add_f32 v[20:21], v[20:21], v[28:29] neg_lo:[0,1] neg_hi:[0,1]
	v_xor_b32_e32 v29, 0x80000000, v20
	v_mov_b32_e32 v28, v21
	v_pk_add_f32 v[20:21], v[22:23], v[30:31]
	v_pk_add_f32 v[22:23], v[22:23], v[30:31] neg_lo:[0,1] neg_hi:[0,1]
	v_pk_mul_f32 v[30:31], v[48:49], v[22:23] op_sel:[0,1] op_sel_hi:[0,0] neg_lo:[1,1] neg_hi:[1,0]
	v_pk_fma_f32 v[22:23], v[48:49], v[22:23], v[30:31] op_sel_hi:[0,1,1] neg_lo:[1,0,0] neg_hi:[1,0,0]
	v_pk_add_f32 v[30:31], v[38:39], v[26:27]
	v_pk_add_f32 v[26:27], v[38:39], v[26:27] neg_lo:[0,1] neg_hi:[0,1]
	v_pk_add_f32 v[38:39], v[40:41], v[20:21]
	v_pk_add_f32 v[20:21], v[40:41], v[20:21] neg_lo:[0,1] neg_hi:[0,1]
	v_mov_b32_e32 v48, v167
	v_xor_b32_e32 v41, 0x80000000, v20
	v_mov_b32_e32 v40, v21
	v_pk_add_f32 v[20:21], v[30:31], v[38:39]
	v_pk_add_f32 v[30:31], v[30:31], v[38:39] neg_lo:[0,1] neg_hi:[0,1]
	v_pk_add_f32 v[38:39], v[26:27], v[40:41]
	v_pk_add_f32 v[26:27], v[26:27], v[40:41] neg_lo:[0,1] neg_hi:[0,1]
	v_pk_add_f32 v[40:41], v[16:17], v[28:29]
	v_pk_add_f32 v[16:17], v[16:17], v[28:29] neg_lo:[0,1] neg_hi:[0,1]
	v_pk_add_f32 v[28:29], v[18:19], v[22:23]
	v_pk_add_f32 v[18:19], v[18:19], v[22:23] neg_lo:[0,1] neg_hi:[0,1]
	v_xor_b32_e32 v23, 0x80000000, v18
	v_mov_b32_e32 v22, v19
	v_pk_add_f32 v[18:19], v[40:41], v[28:29]
	v_pk_add_f32 v[28:29], v[40:41], v[28:29] neg_lo:[0,1] neg_hi:[0,1]
	v_pk_add_f32 v[40:41], v[16:17], v[22:23]
	v_pk_add_f32 v[16:17], v[16:17], v[22:23] neg_lo:[0,1] neg_hi:[0,1]
	v_lshl_add_u64 v[22:23], v[14:15], 3, s[46:47]
	global_store_dwordx2 v[22:23], v[34:35], off
	v_add_u32_e32 v22, 0x200, v14
	v_ashrrev_i32_e32 v23, 31, v22
	v_lshl_add_u64 v[22:23], v[22:23], 3, s[46:47]
	global_store_dwordx2 v[22:23], v[20:21], off
	v_add_u32_e32 v20, 0x400, v14
	v_ashrrev_i32_e32 v21, 31, v20
	v_lshl_add_u64 v[20:21], v[20:21], 3, s[46:47]
	global_store_dwordx2 v[20:21], v[24:25], off
	v_add_u32_e32 v20, 0x600, v14
	v_ashrrev_i32_e32 v21, 31, v20
	v_lshl_add_u64 v[20:21], v[20:21], 3, s[46:47]
	global_store_dwordx2 v[20:21], v[18:19], off
	v_add_u32_e32 v18, 0x800, v14
	v_ashrrev_i32_e32 v19, 31, v18
	v_lshl_add_u64 v[18:19], v[18:19], 3, s[46:47]
	global_store_dwordx2 v[18:19], v[46:47], off
	v_add_u32_e32 v18, 0xa00, v14
	v_ashrrev_i32_e32 v19, 31, v18
	v_lshl_add_u64 v[18:19], v[18:19], 3, s[46:47]
	global_store_dwordx2 v[18:19], v[38:39], off
	v_add_u32_e32 v18, 0xc00, v14
	v_ashrrev_i32_e32 v19, 31, v18
	v_lshl_add_u64 v[18:19], v[18:19], 3, s[46:47]
	global_store_dwordx2 v[18:19], v[50:51], off
	v_add_u32_e32 v18, 0xe00, v14
	v_ashrrev_i32_e32 v19, 31, v18
	v_lshl_add_u64 v[18:19], v[18:19], 3, s[46:47]
	global_store_dwordx2 v[18:19], v[40:41], off
	v_add_u32_e32 v18, 0x1000, v14
	v_ashrrev_i32_e32 v19, 31, v18
	v_lshl_add_u64 v[18:19], v[18:19], 3, s[46:47]
	global_store_dwordx2 v[18:19], v[44:45], off
	v_add_u32_e32 v18, 0x1200, v14
	v_ashrrev_i32_e32 v19, 31, v18
	v_lshl_add_u64 v[18:19], v[18:19], 3, s[46:47]
	global_store_dwordx2 v[18:19], v[30:31], off
	v_add_u32_e32 v18, 0x1400, v14
	v_ashrrev_i32_e32 v19, 31, v18
	v_lshl_add_u64 v[18:19], v[18:19], 3, s[46:47]
	global_store_dwordx2 v[18:19], v[42:43], off
	v_add_u32_e32 v18, 0x1600, v14
	v_ashrrev_i32_e32 v19, 31, v18
	v_lshl_add_u64 v[18:19], v[18:19], 3, s[46:47]
	global_store_dwordx2 v[18:19], v[28:29], off
	v_add_u32_e32 v18, 0x1800, v14
	v_ashrrev_i32_e32 v19, 31, v18
	v_lshl_add_u64 v[18:19], v[18:19], 3, s[46:47]
	global_store_dwordx2 v[18:19], v[32:33], off
	v_add_u32_e32 v18, 0x1a00, v14
	v_ashrrev_i32_e32 v19, 31, v18
	v_lshl_add_u64 v[18:19], v[18:19], 3, s[46:47]
	global_store_dwordx2 v[18:19], v[26:27], off
	v_add_u32_e32 v18, 0x1c00, v14
	v_ashrrev_i32_e32 v19, 31, v18
	v_lshl_add_u64 v[18:19], v[18:19], 3, s[46:47]
	global_store_dwordx2 v[18:19], v[36:37], off
	v_add_u32_e32 v18, 0x1e00, v14
	v_ashrrev_i32_e32 v19, 31, v18
	v_lshl_add_u64 v[18:19], v[18:19], 3, s[46:47]
	global_store_dwordx2 v[18:19], v[16:17], off
	v_mov_b32_e32 v50, v169
	v_xor_b32_e32 v16, 1, v13
	v_lshlrev_b32_e32 v10, 3, v10
	v_lshlrev_b32_e32 v16, 3, v16
	v_add3_u32 v18, 0, v16, v10
	v_xor_b32_e32 v16, 2, v13
	v_lshlrev_b32_e32 v16, 3, v16
	v_xor_b32_e32 v24, 5, v13
	v_add3_u32 v20, 0, v16, v10
	v_xor_b32_e32 v16, 3, v13
	v_lshlrev_b32_e32 v24, 3, v24
	v_lshlrev_b32_e32 v15, 3, v13
	v_lshlrev_b32_e32 v16, 3, v16
	v_add3_u32 v26, 0, v24, v10
	v_xor_b32_e32 v24, 6, v13
	v_add3_u32 v15, 0, v15, v10
	v_add3_u32 v22, 0, v16, v10
	v_lshlrev_b32_e32 v24, 3, v24
	v_xor_b32_e32 v32, 9, v13
	ds_read_b64 v[16:17], v15
	ds_read_b64 v[18:19], v18
	ds_read_b64 v[20:21], v20
	ds_read_b64 v[22:23], v22
	v_xor_b32_e32 v15, 4, v13
	v_add3_u32 v28, 0, v24, v10
	v_xor_b32_e32 v24, 7, v13
	v_lshlrev_b32_e32 v32, 3, v32
	v_lshlrev_b32_e32 v15, 3, v15
	v_lshlrev_b32_e32 v24, 3, v24
	v_add3_u32 v34, 0, v32, v10
	v_xor_b32_e32 v32, 10, v13
	v_add3_u32 v15, 0, v15, v10
	v_add3_u32 v30, 0, v24, v10
	v_lshlrev_b32_e32 v32, 3, v32
	ds_read_b64 v[24:25], v15
	ds_read_b64 v[26:27], v26
	ds_read_b64 v[28:29], v28
	ds_read_b64 v[30:31], v30
	v_xor_b32_e32 v15, 8, v13
	v_add3_u32 v36, 0, v32, v10
	v_xor_b32_e32 v32, 11, v13
	v_lshlrev_b32_e32 v15, 3, v15
	v_lshlrev_b32_e32 v32, 3, v32
	v_xor_b32_e32 v40, 13, v13
	v_add3_u32 v15, 0, v15, v10
	v_add3_u32 v38, 0, v32, v10
	v_lshlrev_b32_e32 v40, 3, v40
	ds_read_b64 v[32:33], v15
	ds_read_b64 v[34:35], v34
	ds_read_b64 v[36:37], v36
	ds_read_b64 v[38:39], v38
	v_xor_b32_e32 v15, 12, v13
	v_add3_u32 v42, 0, v40, v10
	v_xor_b32_e32 v40, 14, v13
	v_xor_b32_e32 v13, 15, v13
	v_lshlrev_b32_e32 v15, 3, v15
	v_lshlrev_b32_e32 v40, 3, v40
	v_lshlrev_b32_e32 v13, 3, v13
	v_add3_u32 v15, 0, v15, v10
	v_add3_u32 v44, 0, v40, v10
	v_add3_u32 v10, 0, v13, v10
	ds_read_b64 v[40:41], v15
	ds_read_b64 v[42:43], v42
	ds_read_b64 v[44:45], v44
	ds_read_b64 v[46:47], v10
	v_mov_b32_e32 v10, v1
	v_mov_b32_e32 v13, v166
	v_mov_b32_e32 v10, v164
	s_waitcnt lgkmcnt(7)
	v_pk_add_f32 v[52:53], v[16:17], v[32:33]
	v_mov_b32_e32 v10, v165
	v_pk_add_f32 v[16:17], v[16:17], v[32:33] neg_lo:[0,1] neg_hi:[0,1]
	s_waitcnt lgkmcnt(6)
	v_pk_add_f32 v[32:33], v[18:19], v[34:35]
	v_pk_add_f32 v[18:19], v[18:19], v[34:35] neg_lo:[0,1] neg_hi:[0,1]
	v_mov_b32_e32 v13, v168
	s_nop 0
	v_pk_mul_f32 v[34:35], v[18:19], v[50:51] op_sel:[1,0] op_sel_hi:[0,0] neg_lo:[1,1] neg_hi:[0,1]
	v_mov_b32_e32 v13, v170
	v_pk_fma_f32 v[18:19], v[18:19], v[10:11], v[34:35] op_sel_hi:[1,0,1]
	s_waitcnt lgkmcnt(5)
	v_pk_add_f32 v[34:35], v[20:21], v[36:37]
	v_pk_add_f32 v[20:21], v[20:21], v[36:37] neg_lo:[0,1] neg_hi:[0,1]
	v_pk_mul_f32 v[36:37], v[20:21], v[48:49] op_sel:[1,0] op_sel_hi:[0,0] neg_lo:[1,1] neg_hi:[0,1]
	v_mov_b32_e32 v13, v171
	v_pk_fma_f32 v[20:21], v[20:21], v[48:49], v[36:37] op_sel_hi:[1,0,1]
	s_waitcnt lgkmcnt(4)
	v_pk_add_f32 v[36:37], v[22:23], v[38:39]
	v_pk_add_f32 v[22:23], v[22:23], v[38:39] neg_lo:[0,1] neg_hi:[0,1]
	v_pk_mul_f32 v[38:39], v[22:23], v[50:51] op_sel_hi:[1,0]
	v_pk_fma_f32 v[22:23], v[22:23], v[10:11], v[38:39] op_sel:[1,0,0] op_sel_hi:[0,0,1] neg_lo:[1,1,0] neg_hi:[0,1,0]
	s_waitcnt lgkmcnt(3)
	v_pk_add_f32 v[38:39], v[24:25], v[40:41]
	v_pk_add_f32 v[24:25], v[24:25], v[40:41] neg_lo:[0,1] neg_hi:[0,1]
	v_mov_b32_e32 v13, v173
	v_xor_b32_e32 v41, 0x80000000, v24
	v_mov_b32_e32 v40, v25
	s_waitcnt lgkmcnt(2)
	v_pk_add_f32 v[24:25], v[26:27], v[42:43]
	v_pk_add_f32 v[26:27], v[26:27], v[42:43] neg_lo:[0,1] neg_hi:[0,1]
	v_pk_mul_f32 v[42:43], v[26:27], v[50:51] op_sel_hi:[1,0] neg_lo:[0,1] neg_hi:[0,1]
	v_pk_fma_f32 v[26:27], v[26:27], v[10:11], v[42:43] op_sel:[1,0,0] op_sel_hi:[0,0,1] neg_lo:[1,1,0] neg_hi:[0,1,0]
	s_waitcnt lgkmcnt(1)
	v_pk_add_f32 v[42:43], v[28:29], v[44:45]
	v_pk_add_f32 v[28:29], v[28:29], v[44:45] neg_lo:[0,1] neg_hi:[0,1]
	v_pk_mul_f32 v[44:45], v[28:29], v[48:49] op_sel:[1,0] op_sel_hi:[0,0] neg_lo:[1,1] neg_hi:[0,1]
	v_pk_fma_f32 v[28:29], v[28:29], v[48:49], v[44:45] op_sel_hi:[1,0,1] neg_lo:[0,1,0] neg_hi:[0,1,0]
	s_waitcnt lgkmcnt(0)
	v_pk_add_f32 v[44:45], v[30:31], v[46:47]
	v_pk_add_f32 v[30:31], v[30:31], v[46:47] neg_lo:[0,1] neg_hi:[0,1]
	v_pk_mul_f32 v[46:47], v[30:31], v[50:51] op_sel:[1,0] op_sel_hi:[0,0] neg_lo:[1,1] neg_hi:[0,1]
	v_pk_add_f32 v[50:51], v[32:33], v[24:25]
	v_pk_add_f32 v[24:25], v[32:33], v[24:25] neg_lo:[0,1] neg_hi:[0,1]
	v_pk_fma_f32 v[30:31], v[30:31], v[10:11], v[46:47] op_sel_hi:[1,0,1] neg_lo:[0,1,0] neg_hi:[0,1,0]
	v_pk_mul_f32 v[32:33], v[24:25], v[48:49] op_sel:[1,0] op_sel_hi:[0,0] neg_lo:[1,1] neg_hi:[0,1]
	v_pk_add_f32 v[46:47], v[52:53], v[38:39]
	v_pk_fma_f32 v[24:25], v[24:25], v[48:49], v[32:33] op_sel_hi:[1,0,1]
	v_pk_add_f32 v[32:33], v[34:35], v[42:43]
	v_pk_add_f32 v[34:35], v[34:35], v[42:43] neg_lo:[0,1] neg_hi:[0,1]
	v_pk_add_f32 v[38:39], v[52:53], v[38:39] neg_lo:[0,1] neg_hi:[0,1]
	v_xor_b32_e32 v43, 0x80000000, v34
	v_mov_b32_e32 v42, v35
	v_pk_add_f32 v[34:35], v[36:37], v[44:45]
	v_pk_add_f32 v[36:37], v[36:37], v[44:45] neg_lo:[0,1] neg_hi:[0,1]
	v_mov_b32_e32 v10, v183
	v_pk_mul_f32 v[44:45], v[36:37], v[48:49] op_sel:[1,0] op_sel_hi:[0,0] neg_lo:[1,1] neg_hi:[0,1]
	v_pk_fma_f32 v[36:37], v[36:37], v[48:49], v[44:45] op_sel_hi:[1,0,1] neg_lo:[0,1,0] neg_hi:[0,1,0]
	v_pk_add_f32 v[44:45], v[46:47], v[32:33]
	v_pk_add_f32 v[32:33], v[46:47], v[32:33] neg_lo:[0,1] neg_hi:[0,1]
	v_pk_add_f32 v[46:47], v[50:51], v[34:35]
	v_pk_add_f32 v[34:35], v[50:51], v[34:35] neg_lo:[0,1] neg_hi:[0,1]
	v_xor_b32_e32 v51, 0x80000000, v34
	v_mov_b32_e32 v50, v35
	v_pk_add_f32 v[34:35], v[44:45], v[46:47]
	v_pk_add_f32 v[44:45], v[44:45], v[46:47] neg_lo:[0,1] neg_hi:[0,1]
	v_pk_add_f32 v[46:47], v[32:33], v[50:51]
	v_pk_add_f32 v[32:33], v[32:33], v[50:51] neg_lo:[0,1] neg_hi:[0,1]
	v_pk_add_f32 v[50:51], v[38:39], v[42:43]
	v_pk_add_f32 v[38:39], v[38:39], v[42:43] neg_lo:[0,1] neg_hi:[0,1]
	v_pk_add_f32 v[42:43], v[24:25], v[36:37]
	v_pk_add_f32 v[24:25], v[24:25], v[36:37] neg_lo:[0,1] neg_hi:[0,1]
	v_xor_b32_e32 v37, 0x80000000, v24
	v_mov_b32_e32 v36, v25
	v_pk_add_f32 v[24:25], v[50:51], v[42:43]
	v_pk_add_f32 v[42:43], v[50:51], v[42:43] neg_lo:[0,1] neg_hi:[0,1]
	v_pk_add_f32 v[50:51], v[38:39], v[36:37]
	v_pk_add_f32 v[36:37], v[38:39], v[36:37] neg_lo:[0,1] neg_hi:[0,1]
	v_pk_add_f32 v[38:39], v[16:17], v[40:41]
	v_pk_add_f32 v[16:17], v[16:17], v[40:41] neg_lo:[0,1] neg_hi:[0,1]
	v_pk_add_f32 v[40:41], v[18:19], v[26:27]
	v_pk_add_f32 v[18:19], v[18:19], v[26:27] neg_lo:[0,1] neg_hi:[0,1]
	v_pk_mul_f32 v[26:27], v[48:49], v[18:19] op_sel:[0,1] op_sel_hi:[0,0] neg_lo:[1,1] neg_hi:[1,0]
	v_pk_fma_f32 v[18:19], v[48:49], v[18:19], v[26:27] op_sel_hi:[0,1,1]
	v_pk_add_f32 v[26:27], v[20:21], v[28:29]
	v_pk_add_f32 v[20:21], v[20:21], v[28:29] neg_lo:[0,1] neg_hi:[0,1]
	v_xor_b32_e32 v29, 0x80000000, v20
	v_mov_b32_e32 v28, v21
	v_pk_add_f32 v[20:21], v[22:23], v[30:31]
	v_pk_add_f32 v[22:23], v[22:23], v[30:31] neg_lo:[0,1] neg_hi:[0,1]
	v_pk_mul_f32 v[30:31], v[48:49], v[22:23] op_sel:[0,1] op_sel_hi:[0,0] neg_lo:[1,1] neg_hi:[1,0]
	v_pk_fma_f32 v[22:23], v[48:49], v[22:23], v[30:31] op_sel_hi:[0,1,1] neg_lo:[1,0,0] neg_hi:[1,0,0]
	v_pk_add_f32 v[30:31], v[38:39], v[26:27]
	v_pk_add_f32 v[26:27], v[38:39], v[26:27] neg_lo:[0,1] neg_hi:[0,1]
	v_pk_add_f32 v[38:39], v[40:41], v[20:21]
	v_pk_add_f32 v[20:21], v[40:41], v[20:21] neg_lo:[0,1] neg_hi:[0,1]
	v_xor_b32_e32 v41, 0x80000000, v20
	v_mov_b32_e32 v40, v21
	v_pk_add_f32 v[20:21], v[30:31], v[38:39]
	v_pk_add_f32 v[30:31], v[30:31], v[38:39] neg_lo:[0,1] neg_hi:[0,1]
	v_pk_add_f32 v[38:39], v[26:27], v[40:41]
	v_pk_add_f32 v[26:27], v[26:27], v[40:41] neg_lo:[0,1] neg_hi:[0,1]
	v_pk_add_f32 v[40:41], v[16:17], v[28:29]
	v_pk_add_f32 v[16:17], v[16:17], v[28:29] neg_lo:[0,1] neg_hi:[0,1]
	v_pk_add_f32 v[28:29], v[18:19], v[22:23]
	v_pk_add_f32 v[18:19], v[18:19], v[22:23] neg_lo:[0,1] neg_hi:[0,1]
	v_xor_b32_e32 v23, 0x80000000, v18
	v_mov_b32_e32 v22, v19
	v_pk_add_f32 v[18:19], v[40:41], v[28:29]
	v_pk_add_f32 v[28:29], v[40:41], v[28:29] neg_lo:[0,1] neg_hi:[0,1]
	v_pk_add_f32 v[40:41], v[16:17], v[22:23]
	v_pk_add_f32 v[16:17], v[16:17], v[22:23] neg_lo:[0,1] neg_hi:[0,1]
	v_add_u32_e32 v22, 0x2000, v14
	v_ashrrev_i32_e32 v23, 31, v22
	v_lshl_add_u64 v[22:23], v[22:23], 3, s[46:47]
	global_store_dwordx2 v[22:23], v[34:35], off
	v_add_u32_e32 v22, 0x2200, v14
	v_ashrrev_i32_e32 v23, 31, v22
	v_lshl_add_u64 v[22:23], v[22:23], 3, s[46:47]
	global_store_dwordx2 v[22:23], v[20:21], off
	v_add_u32_e32 v20, 0x2400, v14
	v_ashrrev_i32_e32 v21, 31, v20
	v_lshl_add_u64 v[20:21], v[20:21], 3, s[46:47]
	global_store_dwordx2 v[20:21], v[24:25], off
	v_add_u32_e32 v20, 0x2600, v14
	v_ashrrev_i32_e32 v21, 31, v20
	v_lshl_add_u64 v[20:21], v[20:21], 3, s[46:47]
	global_store_dwordx2 v[20:21], v[18:19], off
	v_add_u32_e32 v18, 0x2800, v14
	v_ashrrev_i32_e32 v19, 31, v18
	v_lshl_add_u64 v[18:19], v[18:19], 3, s[46:47]
	global_store_dwordx2 v[18:19], v[46:47], off
	v_add_u32_e32 v18, 0x2a00, v14
	v_ashrrev_i32_e32 v19, 31, v18
	v_lshl_add_u64 v[18:19], v[18:19], 3, s[46:47]
	global_store_dwordx2 v[18:19], v[38:39], off
	v_add_u32_e32 v18, 0x2c00, v14
	v_ashrrev_i32_e32 v19, 31, v18
	v_lshl_add_u64 v[18:19], v[18:19], 3, s[46:47]
	global_store_dwordx2 v[18:19], v[50:51], off
	v_add_u32_e32 v18, 0x2e00, v14
	v_ashrrev_i32_e32 v19, 31, v18
	v_lshl_add_u64 v[18:19], v[18:19], 3, s[46:47]
	global_store_dwordx2 v[18:19], v[40:41], off
	v_add_u32_e32 v18, 0x3000, v14
	v_ashrrev_i32_e32 v19, 31, v18
	v_lshl_add_u64 v[18:19], v[18:19], 3, s[46:47]
	global_store_dwordx2 v[18:19], v[44:45], off
	v_add_u32_e32 v18, 0x3200, v14
	v_ashrrev_i32_e32 v19, 31, v18
	v_lshl_add_u64 v[18:19], v[18:19], 3, s[46:47]
	global_store_dwordx2 v[18:19], v[30:31], off
	v_add_u32_e32 v18, 0x3400, v14
	v_ashrrev_i32_e32 v19, 31, v18
	v_lshl_add_u64 v[18:19], v[18:19], 3, s[46:47]
	global_store_dwordx2 v[18:19], v[42:43], off
	v_add_u32_e32 v18, 0x3600, v14
	v_ashrrev_i32_e32 v19, 31, v18
	v_lshl_add_u64 v[18:19], v[18:19], 3, s[46:47]
	global_store_dwordx2 v[18:19], v[28:29], off
	v_add_u32_e32 v18, 0x3800, v14
	v_ashrrev_i32_e32 v19, 31, v18
	v_lshl_add_u64 v[18:19], v[18:19], 3, s[46:47]
	global_store_dwordx2 v[18:19], v[32:33], off
	v_add_u32_e32 v18, 0x3a00, v14
	v_ashrrev_i32_e32 v19, 31, v18
	v_lshl_add_u64 v[18:19], v[18:19], 3, s[46:47]
	global_store_dwordx2 v[18:19], v[26:27], off
	v_add_u32_e32 v18, 0x3c00, v14
	v_add_u32_e32 v14, 0x3e00, v14
	v_ashrrev_i32_e32 v15, 31, v14
	v_ashrrev_i32_e32 v19, 31, v18
	v_lshl_add_u64 v[14:15], v[14:15], 3, s[46:47]
	v_lshl_add_u64 v[18:19], v[18:19], 3, s[46:47]
	global_store_dwordx2 v[14:15], v[16:17], off
	v_mov_b32_e32 v16, v184
	v_mov_b32_e32 v14, v182
	global_store_dwordx2 v[18:19], v[36:37], off
	s_barrier
	s_nop 0
	v_pk_mul_f32 v[36:37], v[16:17], s[64:65] op_sel_hi:[0,1] neg_lo:[1,0]
	s_mov_b64 s[64:65], vcc
	v_ashrrev_i32_e32 v15, 31, v14
	v_lshl_add_u64 v[18:19], v[14:15], 2, s[64:65]
	s_movk_i32 vcc_lo, 0x1000
	v_add_co_u32_e32 v28, vcc, vcc_lo, v18
	v_pk_mul_f32 v[40:41], v[16:17], s[78:79] op_sel_hi:[0,1] neg_lo:[1,0]
	s_nop 0
	v_addc_co_u32_e32 v29, vcc, 0, v19, vcc
	v_add_co_u32_e32 v20, vcc, s39, v18
	s_movk_i32 s78, 0x3000
	s_nop 0
	v_addc_co_u32_e32 v21, vcc, 0, v19, vcc
	v_add_co_u32_e32 v48, vcc, s78, v18
	v_pk_mul_f32 v[32:33], v[16:17], s[40:41] op_sel_hi:[0,1] neg_lo:[1,0]
	s_nop 0
	v_addc_co_u32_e32 v49, vcc, 0, v19, vcc
	v_add_co_u32_e32 v22, vcc, s72, v18
	s_mov_b32 s40, 0x3f7ec46d
	s_nop 0
	v_addc_co_u32_e32 v23, vcc, 0, v19, vcc
	v_add_co_u32_e32 v58, vcc, s33, v18
	s_mov_b32 s33, 0x8000
	s_nop 0
	v_addc_co_u32_e32 v59, vcc, 0, v19, vcc
	v_add_co_u32_e32 v60, vcc, s43, v18
	s_mov_b32 s41, 0xbdc8bd36
	s_nop 0
	v_addc_co_u32_e32 v61, vcc, 0, v19, vcc
	v_add_co_u32_e32 v64, vcc, s73, v18
	v_pk_mul_f32 v[34:35], v[16:17], s[76:77] op_sel_hi:[0,1] neg_lo:[1,0]
	s_nop 0
	v_addc_co_u32_e32 v65, vcc, 0, v19, vcc
	v_add_co_u32_e32 v68, vcc, s33, v18
	s_mov_b32 s33, 0x9000
	s_nop 0
	v_addc_co_u32_e32 v69, vcc, 0, v19, vcc
	v_add_co_u32_e32 v24, vcc, s33, v18
	s_mov_b32 s33, 0xa000
	s_nop 0
	v_addc_co_u32_e32 v25, vcc, 0, v19, vcc
	v_add_co_u32_e32 v26, vcc, s33, v18
	s_mov_b32 s33, 0xb000
	s_nop 0
	v_addc_co_u32_e32 v27, vcc, 0, v19, vcc
	v_add_co_u32_e32 v30, vcc, s33, v18
	s_mov_b32 s33, 0xc000
	s_nop 0
	v_addc_co_u32_e32 v31, vcc, 0, v19, vcc
	v_add_co_u32_e32 v38, vcc, s33, v18
	s_mov_b32 s33, 0xd000
	s_nop 0
	v_addc_co_u32_e32 v39, vcc, 0, v19, vcc
	v_add_co_u32_e32 v44, vcc, s33, v18
	s_mov_b32 s33, 0xe000
	s_nop 0
	v_addc_co_u32_e32 v45, vcc, 0, v19, vcc
	v_add_co_u32_e32 v50, vcc, s33, v18
	s_mov_b32 s33, 0xf000
	s_nop 0
	v_addc_co_u32_e32 v51, vcc, 0, v19, vcc
	v_add_co_u32_e32 v70, vcc, s33, v18
	v_pk_mul_f32 v[92:93], v[16:17], s[62:63] op_sel_hi:[0,1] neg_lo:[1,0]
	s_nop 0
	v_addc_co_u32_e32 v71, vcc, 0, v19, vcc
	global_load_dword v94, v[68:69], off
	global_load_dword v96, v[68:69], off offset:2048
	global_load_dword v98, v[26:27], off offset:-4096
	global_load_dword v100, v[24:25], off offset:2048
	global_load_dword v102, v[26:27], off
	global_load_dword v104, v[26:27], off offset:2048
	global_load_dword v106, v[38:39], off offset:-4096
	global_load_dword v108, v[30:31], off offset:2048
	global_load_dword v110, v[38:39], off
	global_load_dword v112, v[38:39], off offset:2048
	global_load_dword v114, v[50:51], off offset:-4096
	global_load_dword v116, v[44:45], off offset:2048
	global_load_dword v118, v[50:51], off
	global_load_dword v120, v[50:51], off offset:2048
	global_load_dword v122, v[70:71], off
	global_load_dword v56, v[20:21], off
	s_nop 0
	global_load_dword v50, v[20:21], off offset:2048
	global_load_dword v124, v[70:71], off offset:2048
	global_load_dword v44, v[22:23], off offset:-4096
	global_load_dword v38, v[22:23], off
	global_load_dword v72, v[20:21], off offset:-4096
	global_load_dword v30, v[22:23], off offset:2048
	global_load_dword v26, v[60:61], off offset:-4096
	global_load_dword v24, v[60:61], off
	s_nop 0
	global_load_dword v22, v[60:61], off offset:2048
	global_load_dword v20, v[68:69], off offset:-4096
	global_load_dword v74, v[18:19], off
	global_load_dword v78, v[18:19], off offset:2048
	s_nop 0
	global_load_dword v68, v[28:29], off offset:2048
	s_nop 0
	global_load_dword v48, v[48:49], off offset:2048
	s_nop 0
	global_load_dword v28, v[58:59], off offset:2048
	global_load_dword v18, v[64:65], off offset:2048
	v_pk_mul_f32 v[52:53], v[16:17], s[58:59] op_sel_hi:[0,1] neg_lo:[1,0]
	v_pk_fma_f32 v[82:83], v[10:11], s[40:41], v[34:35] op_sel_hi:[0,1,1]
	v_pk_fma_f32 v[34:35], v[10:11], s[92:93], v[92:93] op_sel_hi:[0,1,1]
	s_mov_b32 s92, 0x3e47c5c2
	v_pk_mul_f32 v[66:67], v[16:17], s[60:61] op_sel_hi:[0,1] neg_lo:[1,0]
	v_pk_fma_f32 v[84:85], v[10:11], s[44:45], v[32:33] op_sel_hi:[0,1,1]
	v_pk_fma_f32 v[60:61], v[10:11], s[82:83], v[52:53] op_sel_hi:[0,1,1]
	s_mov_b32 s82, 0x3f45e403
	s_mov_b32 s93, 0xbf7b14be
	v_pk_mul_f32 v[32:33], v[16:17], s[30:31] op_sel_hi:[0,1] neg_lo:[1,0]
	s_mov_b32 s30, 0x3dc8bd36
	v_pk_mul_f32 v[54:55], v[16:17], s[74:75] op_sel_hi:[0,1] neg_lo:[1,0]
	v_pk_mul_f32 v[62:63], v[16:17], s[54:55] op_sel_hi:[0,1] neg_lo:[1,0]
	s_mov_b32 s83, 0xbf226799
	v_pk_fma_f32 v[52:53], v[10:11], s[86:87], v[66:67] op_sel_hi:[0,1,1]
	s_mov_b32 s31, 0xbf7ec46d
	v_pk_fma_f32 v[66:67], v[10:11], s[92:93], v[32:33] op_sel_hi:[0,1,1]
	v_pk_mul_f32 v[32:33], v[16:17], s[34:35] op_sel_hi:[0,1] neg_lo:[1,0]
	v_pk_fma_f32 v[76:77], v[10:11], s[80:81], v[40:41] op_sel_hi:[0,1,1]
	s_mov_b32 s80, 0x3f61c598
	v_pk_fma_f32 v[58:59], v[10:11], s[82:83], v[54:55] op_sel_hi:[0,1,1]
	v_pk_fma_f32 v[54:55], v[10:11], s[84:85], v[62:63] op_sel_hi:[0,1,1]
	s_mov_b32 s86, 0x3f0e39da
	v_pk_fma_f32 v[62:63], v[10:11], s[30:31], v[32:33] op_sel_hi:[0,1,1]
	v_pk_mul_f32 v[32:33], v[16:17], s[36:37] op_sel_hi:[0,1] neg_lo:[1,0]
	v_pk_mul_f32 v[46:47], v[16:17], s[48:49] op_sel_hi:[0,1] neg_lo:[1,0]
	v_pk_mul_f32 v[86:87], v[16:17], s[66:67] op_sel_hi:[0,1] neg_lo:[1,0]
	s_mov_b32 s81, 0xbef15aea
	s_mov_b32 s87, 0xbf54db31
	v_pk_fma_f32 v[32:33], v[10:11], s[96:97], v[32:33] op_sel_hi:[0,1,1]
	s_mov_b32 s54, 0x3f6c835e
	v_pk_fma_f32 v[64:65], v[10:11], s[80:81], v[46:47] op_sel_hi:[0,1,1]
	v_pk_fma_f32 v[46:47], v[10:11], s[86:87], v[86:87] op_sel_hi:[0,1,1]
	v_pk_mul_f32 v[42:43], v[16:17], s[50:51] op_sel_hi:[0,1] neg_lo:[1,0]
	v_pk_mul_f32 v[88:89], v[16:17], s[68:69] op_sel_hi:[0,1] neg_lo:[1,0]
	s_mov_b32 s55, 0xbec3ef15
	v_pk_fma_f32 v[70:71], v[10:11], s[54:55], v[42:43] op_sel_hi:[0,1,1]
	v_pk_fma_f32 v[42:43], v[10:11], s[88:89], v[88:89] op_sel_hi:[0,1,1]
	s_mov_b32 s88, 0x3ec3ef15
	v_pk_mul_f32 v[90:91], v[16:17], s[56:57] op_sel_hi:[0,1] neg_lo:[1,0]
	s_mov_b32 s89, 0xbf6c835e
	v_pk_fma_f32 v[40:41], v[10:11], s[88:89], v[90:91] op_sel_hi:[0,1,1]
	s_mov_b32 s76, 0x3f7b14be
	s_mov_b32 s77, 0xbe47c5c2
	v_pk_fma_f32 v[80:81], v[10:11], s[76:77], v[36:37] op_sel_hi:[0,1,1]
	v_mov_b32_e32 v36, v169
	v_mov_b32_e32 v15, v171
	s_waitcnt vmcnt(31)
	v_pk_mul_f32 v[86:87], v[32:33], v[94:95] op_sel_hi:[1,0]
	v_pk_mul_f32 v[32:33], v[16:17], s[2:3] op_sel_hi:[0,1] neg_lo:[1,0]
	v_pk_fma_f32 v[32:33], v[10:11], s[0:1], v[32:33] op_sel_hi:[0,1,1]
	s_waitcnt vmcnt(30)
	v_pk_mul_f32 v[88:89], v[32:33], v[96:97] op_sel_hi:[1,0]
	v_pk_mul_f32 v[32:33], v[16:17], s[6:7] op_sel_hi:[0,1] neg_lo:[1,0]
	v_pk_fma_f32 v[32:33], v[10:11], s[4:5], v[32:33] op_sel_hi:[0,1,1]
	s_waitcnt vmcnt(29)
	v_pk_mul_f32 v[90:91], v[32:33], v[98:99] op_sel_hi:[1,0]
	v_pk_mul_f32 v[32:33], v[16:17], s[10:11] op_sel_hi:[0,1] neg_lo:[1,0]
	v_pk_fma_f32 v[32:33], v[10:11], s[8:9], v[32:33] op_sel_hi:[0,1,1]
	s_waitcnt vmcnt(28)
	v_pk_mul_f32 v[92:93], v[32:33], v[100:101] op_sel_hi:[1,0]
	v_pk_mul_f32 v[32:33], v[16:17], s[16:17] op_sel_hi:[0,1] neg_lo:[1,0]
	v_pk_fma_f32 v[32:33], v[10:11], s[12:13], v[32:33] op_sel_hi:[0,1,1]
	s_waitcnt vmcnt(27)
	v_pk_mul_f32 v[94:95], v[32:33], v[102:103] op_sel_hi:[1,0]
	v_pk_mul_f32 v[32:33], v[16:17], s[20:21] op_sel_hi:[0,1] neg_lo:[1,0]
	v_pk_fma_f32 v[32:33], v[10:11], s[18:19], v[32:33] op_sel_hi:[0,1,1]
	s_waitcnt vmcnt(26)
	v_pk_mul_f32 v[96:97], v[32:33], v[104:105] op_sel_hi:[1,0]
	v_pk_mul_f32 v[32:33], v[16:17], s[24:25] op_sel_hi:[0,1] neg_lo:[1,0]
	v_pk_fma_f32 v[32:33], v[10:11], s[22:23], v[32:33] op_sel_hi:[0,1,1]
	s_waitcnt vmcnt(25)
	v_pk_mul_f32 v[98:99], v[32:33], v[106:107] op_sel_hi:[1,0]
	v_pk_mul_f32 v[32:33], v[16:17], s[28:29] op_sel_hi:[0,1] neg_lo:[1,0]
	v_pk_fma_f32 v[32:33], v[10:11], s[26:27], v[32:33] op_sel_hi:[0,1,1]
	s_waitcnt vmcnt(24)
	v_pk_mul_f32 v[100:101], v[32:33], v[108:109] op_sel_hi:[1,0]
	v_pk_mul_f32 v[32:33], v[16:17], s[84:85] op_sel_hi:[0,0] neg_lo:[1,0]
	v_pk_fma_f32 v[32:33], v[10:11], s[38:39], v[32:33] op_sel_hi:[0,0,1] neg_lo:[0,0,1] neg_hi:[0,0,1]
	s_waitcnt vmcnt(23)
	v_pk_mul_f32 v[102:103], v[32:33], v[110:111] op_sel_hi:[1,0]
	v_pk_mul_f32 v[32:33], v[16:17], s[26:27] op_sel_hi:[0,1] neg_lo:[1,0]
	v_pk_fma_f32 v[32:33], v[10:11], s[28:29], v[32:33] op_sel_hi:[0,1,1]
	s_waitcnt vmcnt(22)
	v_pk_mul_f32 v[104:105], v[32:33], v[112:113] op_sel_hi:[1,0]
	v_pk_mul_f32 v[32:33], v[16:17], s[22:23] op_sel_hi:[0,1] neg_lo:[1,0]
	v_pk_fma_f32 v[32:33], v[10:11], s[24:25], v[32:33] op_sel_hi:[0,1,1]
	s_waitcnt vmcnt(21)
	v_pk_mul_f32 v[106:107], v[32:33], v[114:115] op_sel_hi:[1,0]
	v_pk_mul_f32 v[32:33], v[16:17], s[18:19] op_sel_hi:[0,1] neg_lo:[1,0]
	v_pk_fma_f32 v[32:33], v[10:11], s[20:21], v[32:33] op_sel_hi:[0,1,1]
	s_waitcnt vmcnt(20)
	v_pk_mul_f32 v[108:109], v[32:33], v[116:117] op_sel_hi:[1,0]
	v_pk_mul_f32 v[32:33], v[16:17], s[12:13] op_sel_hi:[0,1] neg_lo:[1,0]
	v_pk_fma_f32 v[32:33], v[10:11], s[16:17], v[32:33] op_sel_hi:[0,1,1]
	s_waitcnt vmcnt(19)
	v_pk_mul_f32 v[110:111], v[32:33], v[118:119] op_sel_hi:[1,0]
	v_pk_mul_f32 v[32:33], v[16:17], s[8:9] op_sel_hi:[0,1] neg_lo:[1,0]
	v_pk_fma_f32 v[32:33], v[10:11], s[10:11], v[32:33] op_sel_hi:[0,1,1]
	s_waitcnt vmcnt(18)
	v_pk_mul_f32 v[112:113], v[32:33], v[120:121] op_sel_hi:[1,0]
	v_pk_mul_f32 v[32:33], v[16:17], s[4:5] op_sel_hi:[0,1] neg_lo:[1,0]
	v_pk_mul_f32 v[16:17], v[16:17], s[0:1] op_sel_hi:[0,1] neg_lo:[1,0]
	v_pk_fma_f32 v[16:17], v[10:11], s[2:3], v[16:17] op_sel_hi:[0,1,1]
	v_pk_fma_f32 v[32:33], v[10:11], s[6:7], v[32:33] op_sel_hi:[0,1,1]
	s_waitcnt vmcnt(14)
	v_pk_mul_f32 v[116:117], v[16:17], v[124:125] op_sel_hi:[1,0]
	v_mov_b32_e32 v10, v1
	s_waitcnt vmcnt(5)
	v_pk_fma_f32 v[126:127], v[74:75], v[84:85], v[86:87] op_sel_hi:[0,1,1]
	v_pk_fma_f32 v[74:75], v[74:75], v[84:85], v[86:87] op_sel_hi:[0,1,1] neg_lo:[0,0,1] neg_hi:[0,0,1]
	s_waitcnt vmcnt(4)
	v_pk_fma_f32 v[84:85], v[82:83], v[78:79], v[88:89] op_sel_hi:[1,0,1]
	v_pk_fma_f32 v[78:79], v[82:83], v[78:79], v[88:89] op_sel_hi:[1,0,1] neg_lo:[0,0,1] neg_hi:[0,0,1]
	v_pk_mul_f32 v[114:115], v[32:33], v[122:123] op_sel_hi:[1,0]
	v_mov_b32_e32 v118, v164
	v_mov_b32_e32 v32, v165
	v_mov_b32_e32 v120, v166
	v_mov_b32_e32 v10, v167
	v_mov_b32_e32 v122, v168
	v_mov_b32_e32 v124, v170
	s_nop 0
	v_pk_mul_f32 v[82:83], v[78:79], v[124:125] op_sel:[1,0] op_sel_hi:[0,0] neg_lo:[1,1] neg_hi:[0,1]
	v_pk_fma_f32 v[78:79], v[78:79], v[118:119], v[82:83] op_sel_hi:[1,0,1]
	v_pk_fma_f32 v[82:83], v[80:81], v[72:73], v[90:91] op_sel_hi:[1,0,1]
	v_pk_fma_f32 v[72:73], v[80:81], v[72:73], v[90:91] op_sel_hi:[1,0,1] neg_lo:[0,0,1] neg_hi:[0,0,1]
	v_pk_mul_f32 v[80:81], v[72:73], v[36:37] op_sel:[1,0] op_sel_hi:[0,0] neg_lo:[1,1] neg_hi:[0,1]
	v_pk_fma_f32 v[72:73], v[72:73], v[32:33], v[80:81] op_sel_hi:[1,0,1]
	s_waitcnt vmcnt(3)
	v_pk_fma_f32 v[80:81], v[76:77], v[68:69], v[92:93] op_sel_hi:[1,0,1]
	v_pk_fma_f32 v[68:69], v[76:77], v[68:69], v[92:93] op_sel_hi:[1,0,1] neg_lo:[0,0,1] neg_hi:[0,0,1]
	v_pk_mul_f32 v[76:77], v[68:69], v[122:123] op_sel:[1,0] op_sel_hi:[0,0] neg_lo:[1,1] neg_hi:[0,1]
	v_pk_fma_f32 v[68:69], v[68:69], v[120:121], v[76:77] op_sel_hi:[1,0,1]
	v_pk_fma_f32 v[76:77], v[70:71], v[56:57], v[94:95] op_sel_hi:[1,0,1]
	v_pk_fma_f32 v[56:57], v[70:71], v[56:57], v[94:95] op_sel_hi:[1,0,1] neg_lo:[0,0,1] neg_hi:[0,0,1]
	v_pk_mul_f32 v[70:71], v[56:57], v[10:11] op_sel:[1,0] op_sel_hi:[0,0] neg_lo:[1,1] neg_hi:[0,1]
	v_pk_fma_f32 v[56:57], v[56:57], v[10:11], v[70:71] op_sel_hi:[1,0,1]
	v_pk_fma_f32 v[70:71], v[64:65], v[50:51], v[96:97] op_sel_hi:[1,0,1]
	v_pk_fma_f32 v[50:51], v[64:65], v[50:51], v[96:97] op_sel_hi:[1,0,1] neg_lo:[0,0,1] neg_hi:[0,0,1]
	v_pk_mul_f32 v[64:65], v[50:51], v[122:123] op_sel_hi:[1,0]
	v_xor_b32_e32 v86, 0x80000000, v51
	v_mov_b32_e32 v87, v50
	v_pk_fma_f32 v[50:51], v[60:61], v[44:45], v[98:99] op_sel_hi:[1,0,1]
	v_pk_fma_f32 v[44:45], v[60:61], v[44:45], v[98:99] op_sel_hi:[1,0,1] neg_lo:[0,0,1] neg_hi:[0,0,1]
	v_pk_fma_f32 v[64:65], v[86:87], v[120:121], v[64:65] op_sel_hi:[1,0,1] neg_lo:[0,1,0] neg_hi:[0,1,0]
	v_pk_mul_f32 v[60:61], v[44:45], v[36:37] op_sel_hi:[1,0]
	v_xor_b32_e32 v86, 0x80000000, v45
	v_mov_b32_e32 v87, v44
	s_waitcnt vmcnt(2)
	v_pk_fma_f32 v[44:45], v[58:59], v[48:49], v[100:101] op_sel_hi:[1,0,1]
	v_pk_fma_f32 v[48:49], v[58:59], v[48:49], v[100:101] op_sel_hi:[1,0,1] neg_lo:[0,0,1] neg_hi:[0,0,1]
	v_pk_fma_f32 v[60:61], v[86:87], v[32:33], v[60:61] op_sel_hi:[1,0,1] neg_lo:[0,1,0] neg_hi:[0,1,0]
	v_pk_mul_f32 v[58:59], v[48:49], v[124:125] op_sel_hi:[1,0]
	v_pk_fma_f32 v[48:49], v[48:49], v[118:119], v[58:59] op_sel:[1,0,0] op_sel_hi:[0,0,1] neg_lo:[1,1,0] neg_hi:[0,1,0]
	v_pk_fma_f32 v[58:59], v[54:55], v[38:39], v[102:103] op_sel_hi:[1,0,1]
	v_pk_fma_f32 v[38:39], v[54:55], v[38:39], v[102:103] op_sel_hi:[1,0,1] neg_lo:[0,0,1] neg_hi:[0,0,1]
	v_xor_b32_e32 v55, 0x80000000, v38
	v_mov_b32_e32 v54, v39
	v_pk_fma_f32 v[38:39], v[52:53], v[30:31], v[104:105] op_sel_hi:[1,0,1]
	v_pk_fma_f32 v[30:31], v[52:53], v[30:31], v[104:105] op_sel_hi:[1,0,1] neg_lo:[0,0,1] neg_hi:[0,0,1]
	v_pk_mul_f32 v[52:53], v[30:31], v[124:125] op_sel_hi:[1,0] neg_lo:[0,1] neg_hi:[0,1]
	v_xor_b32_e32 v86, 0x80000000, v31
	v_mov_b32_e32 v87, v30
	v_pk_fma_f32 v[30:31], v[46:47], v[26:27], v[106:107] op_sel_hi:[1,0,1]
	v_pk_fma_f32 v[26:27], v[46:47], v[26:27], v[106:107] op_sel_hi:[1,0,1] neg_lo:[0,0,1] neg_hi:[0,0,1]
	v_pk_fma_f32 v[52:53], v[86:87], v[118:119], v[52:53] op_sel_hi:[1,0,1] neg_lo:[0,1,0] neg_hi:[0,1,0]
	v_pk_mul_f32 v[46:47], v[26:27], v[36:37] op_sel_hi:[1,0] neg_lo:[0,1] neg_hi:[0,1]
	v_xor_b32_e32 v86, 0x80000000, v27
	v_mov_b32_e32 v87, v26
	s_waitcnt vmcnt(1)
	v_pk_fma_f32 v[26:27], v[42:43], v[28:29], v[108:109] op_sel_hi:[1,0,1]
	v_pk_fma_f32 v[28:29], v[42:43], v[28:29], v[108:109] op_sel_hi:[1,0,1] neg_lo:[0,0,1] neg_hi:[0,0,1]
	v_pk_fma_f32 v[86:87], v[86:87], v[32:33], v[46:47] op_sel_hi:[1,0,1] neg_lo:[0,1,0] neg_hi:[0,1,0]
	v_pk_mul_f32 v[42:43], v[28:29], v[122:123] op_sel_hi:[1,0] neg_lo:[0,1] neg_hi:[0,1]
	v_xor_b32_e32 v46, 0x80000000, v29
	v_mov_b32_e32 v47, v28
	v_pk_fma_f32 v[28:29], v[40:41], v[24:25], v[110:111] op_sel_hi:[1,0,1]
	v_pk_fma_f32 v[24:25], v[40:41], v[24:25], v[110:111] op_sel_hi:[1,0,1] neg_lo:[0,0,1] neg_hi:[0,0,1]
	v_pk_fma_f32 v[42:43], v[46:47], v[120:121], v[42:43] op_sel_hi:[1,0,1] neg_lo:[0,1,0] neg_hi:[0,1,0]
	v_pk_mul_f32 v[40:41], v[24:25], v[10:11] op_sel:[1,0] op_sel_hi:[0,0] neg_lo:[1,1] neg_hi:[0,1]
	v_pk_fma_f32 v[88:89], v[24:25], v[10:11], v[40:41] op_sel_hi:[1,0,1] neg_lo:[0,1,0] neg_hi:[0,1,0]
	v_pk_fma_f32 v[24:25], v[34:35], v[22:23], v[112:113] op_sel_hi:[1,0,1]
	v_pk_fma_f32 v[22:23], v[34:35], v[22:23], v[112:113] op_sel_hi:[1,0,1] neg_lo:[0,0,1] neg_hi:[0,0,1]
	v_pk_add_f32 v[40:41], v[84:85], v[38:39]
	v_pk_mul_f32 v[34:35], v[22:23], v[122:123] op_sel:[1,0] op_sel_hi:[0,0] neg_lo:[1,1] neg_hi:[0,1]
	v_pk_add_f32 v[38:39], v[84:85], v[38:39] neg_lo:[0,1] neg_hi:[0,1]
	v_pk_fma_f32 v[90:91], v[22:23], v[120:121], v[34:35] op_sel_hi:[1,0,1] neg_lo:[0,1,0] neg_hi:[0,1,0]
	v_pk_fma_f32 v[22:23], v[66:67], v[20:21], v[114:115] op_sel_hi:[1,0,1]
	v_pk_fma_f32 v[20:21], v[66:67], v[20:21], v[114:115] op_sel_hi:[1,0,1] neg_lo:[0,0,1] neg_hi:[0,0,1]
	v_pk_mul_f32 v[34:35], v[20:21], v[36:37] op_sel:[1,0] op_sel_hi:[0,0] neg_lo:[1,1] neg_hi:[0,1]
	v_pk_fma_f32 v[66:67], v[20:21], v[32:33], v[34:35] op_sel_hi:[1,0,1] neg_lo:[0,1,0] neg_hi:[0,1,0]
	s_waitcnt vmcnt(0)
	v_pk_fma_f32 v[20:21], v[62:63], v[18:19], v[116:117] op_sel_hi:[1,0,1]
	v_pk_fma_f32 v[18:19], v[62:63], v[18:19], v[116:117] op_sel_hi:[1,0,1] neg_lo:[0,0,1] neg_hi:[0,0,1]
	v_pk_mul_f32 v[46:47], v[38:39], v[36:37] op_sel:[1,0] op_sel_hi:[0,0] neg_lo:[1,1] neg_hi:[0,1]
	v_pk_mul_f32 v[34:35], v[18:19], v[124:125] op_sel:[1,0] op_sel_hi:[0,0] neg_lo:[1,1] neg_hi:[0,1]
	v_pk_fma_f32 v[38:39], v[38:39], v[32:33], v[46:47] op_sel_hi:[1,0,1]
	v_pk_add_f32 v[46:47], v[82:83], v[30:31]
	v_pk_add_f32 v[30:31], v[82:83], v[30:31] neg_lo:[0,1] neg_hi:[0,1]
	v_pk_fma_f32 v[62:63], v[18:19], v[118:119], v[34:35] op_sel_hi:[1,0,1] neg_lo:[0,1,0] neg_hi:[0,1,0]
	v_pk_add_f32 v[18:19], v[126:127], v[58:59]
	v_pk_add_f32 v[34:35], v[126:127], v[58:59] neg_lo:[0,1] neg_hi:[0,1]
	v_pk_mul_f32 v[58:59], v[30:31], v[10:11] op_sel:[1,0] op_sel_hi:[0,0] neg_lo:[1,1] neg_hi:[0,1]
	v_pk_fma_f32 v[58:59], v[30:31], v[10:11], v[58:59] op_sel_hi:[1,0,1]
	v_pk_add_f32 v[30:31], v[80:81], v[26:27]
	v_pk_add_f32 v[26:27], v[80:81], v[26:27] neg_lo:[0,1] neg_hi:[0,1]
	v_pk_mul_f32 v[80:81], v[26:27], v[36:37] op_sel_hi:[1,0]
	v_xor_b32_e32 v82, 0x80000000, v27
	v_mov_b32_e32 v83, v26
	v_pk_add_f32 v[26:27], v[76:77], v[28:29]
	v_pk_add_f32 v[28:29], v[76:77], v[28:29] neg_lo:[0,1] neg_hi:[0,1]
	v_pk_fma_f32 v[80:81], v[82:83], v[32:33], v[80:81] op_sel_hi:[1,0,1] neg_lo:[0,1,0] neg_hi:[0,1,0]
	v_xor_b32_e32 v77, 0x80000000, v28
	v_mov_b32_e32 v76, v29
	v_pk_add_f32 v[28:29], v[70:71], v[24:25]
	v_pk_add_f32 v[24:25], v[70:71], v[24:25] neg_lo:[0,1] neg_hi:[0,1]
	v_pk_mul_f32 v[70:71], v[24:25], v[36:37] op_sel_hi:[1,0] neg_lo:[0,1] neg_hi:[0,1]
	v_pk_fma_f32 v[24:25], v[24:25], v[32:33], v[70:71] op_sel:[1,0,0] op_sel_hi:[0,0,1] neg_lo:[1,1,0] neg_hi:[0,1,0]
	v_pk_add_f32 v[70:71], v[50:51], v[22:23]
	v_pk_add_f32 v[22:23], v[50:51], v[22:23] neg_lo:[0,1] neg_hi:[0,1]
	v_pk_mul_f32 v[50:51], v[22:23], v[10:11] op_sel:[1,0] op_sel_hi:[0,0] neg_lo:[1,1] neg_hi:[0,1]
	v_pk_fma_f32 v[50:51], v[22:23], v[10:11], v[50:51] op_sel_hi:[1,0,1] neg_lo:[0,1,0] neg_hi:[0,1,0]
	v_pk_add_f32 v[22:23], v[44:45], v[20:21]
	v_pk_add_f32 v[20:21], v[44:45], v[20:21] neg_lo:[0,1] neg_hi:[0,1]
	v_pk_mul_f32 v[44:45], v[20:21], v[36:37] op_sel:[1,0] op_sel_hi:[0,0] neg_lo:[1,1] neg_hi:[0,1]
	v_pk_fma_f32 v[20:21], v[20:21], v[32:33], v[44:45] op_sel_hi:[1,0,1] neg_lo:[0,1,0] neg_hi:[0,1,0]
	v_pk_add_f32 v[44:45], v[18:19], v[26:27]
	v_pk_add_f32 v[18:19], v[18:19], v[26:27] neg_lo:[0,1] neg_hi:[0,1]
	v_pk_add_f32 v[26:27], v[40:41], v[28:29]
	v_pk_add_f32 v[28:29], v[40:41], v[28:29] neg_lo:[0,1] neg_hi:[0,1]
	v_pk_mul_f32 v[40:41], v[28:29], v[10:11] op_sel:[1,0] op_sel_hi:[0,0] neg_lo:[1,1] neg_hi:[0,1]
	v_pk_fma_f32 v[28:29], v[28:29], v[10:11], v[40:41] op_sel_hi:[1,0,1]
	v_pk_add_f32 v[40:41], v[46:47], v[70:71]
	v_pk_add_f32 v[46:47], v[46:47], v[70:71] neg_lo:[0,1] neg_hi:[0,1]
	v_xor_b32_e32 v71, 0x80000000, v46
	v_mov_b32_e32 v70, v47
	v_pk_add_f32 v[46:47], v[30:31], v[22:23]
	v_pk_add_f32 v[22:23], v[30:31], v[22:23] neg_lo:[0,1] neg_hi:[0,1]
	v_pk_mul_f32 v[30:31], v[22:23], v[10:11] op_sel:[1,0] op_sel_hi:[0,0] neg_lo:[1,1] neg_hi:[0,1]
	v_pk_fma_f32 v[82:83], v[22:23], v[10:11], v[30:31] op_sel_hi:[1,0,1] neg_lo:[0,1,0] neg_hi:[0,1,0]
	v_pk_add_f32 v[30:31], v[26:27], v[46:47]
	v_pk_add_f32 v[26:27], v[26:27], v[46:47] neg_lo:[0,1] neg_hi:[0,1]
	v_pk_add_f32 v[22:23], v[44:45], v[40:41]
	v_pk_add_f32 v[40:41], v[44:45], v[40:41] neg_lo:[0,1] neg_hi:[0,1]
	v_pk_add_f32 v[84:85], v[22:23], v[30:31]
	v_pk_add_f32 v[30:31], v[22:23], v[30:31] neg_lo:[0,1] neg_hi:[0,1]
	v_pk_add_f32 v[46:47], v[40:41], v[26:27] op_sel:[0,1] op_sel_hi:[1,0] neg_hi:[0,1]
	v_pk_add_f32 v[22:23], v[40:41], v[26:27] op_sel:[0,1] op_sel_hi:[1,0] neg_lo:[0,1]
	v_pk_add_f32 v[40:41], v[28:29], v[82:83]
	v_pk_add_f32 v[28:29], v[28:29], v[82:83] neg_lo:[0,1] neg_hi:[0,1]
	v_pk_add_f32 v[26:27], v[18:19], v[70:71]
	v_pk_add_f32 v[18:19], v[18:19], v[70:71] neg_lo:[0,1] neg_hi:[0,1]
	v_pk_add_f32 v[70:71], v[26:27], v[40:41]
	v_pk_add_f32 v[26:27], v[26:27], v[40:41] neg_lo:[0,1] neg_hi:[0,1]
	v_pk_add_f32 v[40:41], v[18:19], v[28:29] op_sel:[0,1] op_sel_hi:[1,0] neg_hi:[0,1]
	v_pk_add_f32 v[18:19], v[18:19], v[28:29] op_sel:[0,1] op_sel_hi:[1,0] neg_lo:[0,1]
	v_pk_add_f32 v[28:29], v[34:35], v[76:77]
	v_pk_add_f32 v[44:45], v[34:35], v[76:77] neg_lo:[0,1] neg_hi:[0,1]
	v_pk_add_f32 v[34:35], v[38:39], v[24:25]
	v_pk_add_f32 v[24:25], v[38:39], v[24:25] neg_lo:[0,1] neg_hi:[0,1]
	v_pk_mul_f32 v[38:39], v[10:11], v[24:25] op_sel:[0,1] op_sel_hi:[0,0] neg_lo:[1,1] neg_hi:[1,0]
	v_pk_fma_f32 v[38:39], v[10:11], v[24:25], v[38:39] op_sel_hi:[0,1,1]
	v_pk_add_f32 v[24:25], v[58:59], v[50:51]
	v_pk_add_f32 v[50:51], v[58:59], v[50:51] neg_lo:[0,1] neg_hi:[0,1]
	v_xor_b32_e32 v59, 0x80000000, v50
	v_mov_b32_e32 v58, v51
	v_pk_add_f32 v[50:51], v[80:81], v[20:21]
	v_pk_add_f32 v[20:21], v[80:81], v[20:21] neg_lo:[0,1] neg_hi:[0,1]
	v_pk_mul_f32 v[76:77], v[10:11], v[20:21] op_sel:[0,1] op_sel_hi:[0,0] neg_lo:[1,1] neg_hi:[1,0]
	v_pk_fma_f32 v[20:21], v[10:11], v[20:21], v[76:77] op_sel_hi:[0,1,1] neg_lo:[1,0,0] neg_hi:[1,0,0]
	v_pk_add_f32 v[76:77], v[28:29], v[24:25]
	v_pk_add_f32 v[24:25], v[28:29], v[24:25] neg_lo:[0,1] neg_hi:[0,1]
	v_pk_add_f32 v[28:29], v[34:35], v[50:51]
	v_pk_add_f32 v[34:35], v[34:35], v[50:51] neg_lo:[0,1] neg_hi:[0,1]
	v_pk_add_f32 v[82:83], v[76:77], v[28:29]
	v_xor_b32_e32 v81, 0x80000000, v34
	v_mov_b32_e32 v80, v35
	v_pk_add_f32 v[34:35], v[76:77], v[28:29] neg_lo:[0,1] neg_hi:[0,1]
	v_pk_add_f32 v[28:29], v[44:45], v[58:59]
	v_pk_add_f32 v[58:59], v[44:45], v[58:59] neg_lo:[0,1] neg_hi:[0,1]
	v_pk_add_f32 v[44:45], v[38:39], v[20:21]
	v_pk_add_f32 v[20:21], v[38:39], v[20:21] neg_lo:[0,1] neg_hi:[0,1]
	v_pk_add_f32 v[76:77], v[28:29], v[44:45]
	v_pk_add_f32 v[28:29], v[28:29], v[44:45] neg_lo:[0,1] neg_hi:[0,1]
	v_pk_add_f32 v[44:45], v[58:59], v[20:21] op_sel:[0,1] op_sel_hi:[1,0] neg_hi:[0,1]
	v_pk_add_f32 v[20:21], v[58:59], v[20:21] op_sel:[0,1] op_sel_hi:[1,0] neg_lo:[0,1]
	v_pk_add_f32 v[38:39], v[74:75], v[54:55]
	v_pk_add_f32 v[58:59], v[74:75], v[54:55] neg_lo:[0,1] neg_hi:[0,1]
	v_pk_add_f32 v[54:55], v[78:79], v[52:53]
	v_pk_add_f32 v[52:53], v[78:79], v[52:53] neg_lo:[0,1] neg_hi:[0,1]
	v_pk_add_f32 v[50:51], v[24:25], v[80:81]
	v_pk_mul_f32 v[74:75], v[36:37], v[52:53] op_sel:[0,1] op_sel_hi:[0,0] neg_lo:[1,1] neg_hi:[1,0]
	v_pk_fma_f32 v[52:53], v[32:33], v[52:53], v[74:75] op_sel_hi:[0,1,1]
	v_pk_add_f32 v[74:75], v[72:73], v[86:87]
	v_pk_add_f32 v[72:73], v[72:73], v[86:87] neg_lo:[0,1] neg_hi:[0,1]
	v_pk_add_f32 v[24:25], v[24:25], v[80:81] neg_lo:[0,1] neg_hi:[0,1]
	v_pk_mul_f32 v[78:79], v[10:11], v[72:73] op_sel:[0,1] op_sel_hi:[0,0] neg_lo:[1,1] neg_hi:[1,0]
	v_pk_fma_f32 v[72:73], v[10:11], v[72:73], v[78:79] op_sel_hi:[0,1,1]
	v_pk_add_f32 v[78:79], v[68:69], v[42:43]
	v_pk_add_f32 v[42:43], v[68:69], v[42:43] neg_lo:[0,1] neg_hi:[0,1]
	v_pk_mul_f32 v[68:69], v[32:33], v[42:43] op_sel:[0,1] op_sel_hi:[0,0] neg_lo:[1,1] neg_hi:[1,0]
	v_pk_fma_f32 v[42:43], v[36:37], v[42:43], v[68:69] op_sel_hi:[0,1,1]
	v_pk_add_f32 v[68:69], v[56:57], v[88:89]
	v_pk_add_f32 v[56:57], v[56:57], v[88:89] neg_lo:[0,1] neg_hi:[0,1]
	v_xor_b32_e32 v81, 0x80000000, v56
	v_mov_b32_e32 v80, v57
	v_pk_add_f32 v[56:57], v[64:65], v[90:91]
	v_pk_add_f32 v[64:65], v[64:65], v[90:91] neg_lo:[0,1] neg_hi:[0,1]
	v_pk_mul_f32 v[86:87], v[32:33], v[64:65] op_sel:[0,1] op_sel_hi:[0,0] neg_lo:[1,1] neg_hi:[1,0]
	v_pk_fma_f32 v[64:65], v[36:37], v[64:65], v[86:87] op_sel_hi:[0,1,1] neg_lo:[1,0,0] neg_hi:[1,0,0]
	v_pk_add_f32 v[86:87], v[60:61], v[66:67]
	v_pk_add_f32 v[60:61], v[60:61], v[66:67] neg_lo:[0,1] neg_hi:[0,1]
	v_pk_mul_f32 v[66:67], v[10:11], v[60:61] op_sel:[0,1] op_sel_hi:[0,0] neg_lo:[1,1] neg_hi:[1,0]
	v_pk_fma_f32 v[60:61], v[10:11], v[60:61], v[66:67] op_sel_hi:[0,1,1] neg_lo:[1,0,0] neg_hi:[1,0,0]
	v_pk_add_f32 v[66:67], v[48:49], v[62:63]
	v_pk_add_f32 v[48:49], v[48:49], v[62:63] neg_lo:[0,1] neg_hi:[0,1]
	v_pk_mul_f32 v[36:37], v[36:37], v[48:49] op_sel:[0,1] op_sel_hi:[0,0] neg_lo:[1,1] neg_hi:[1,0]
	v_pk_fma_f32 v[36:37], v[32:33], v[48:49], v[36:37] op_sel_hi:[0,1,1] neg_lo:[1,0,0] neg_hi:[1,0,0]
	v_pk_add_f32 v[32:33], v[38:39], v[68:69]
	v_pk_add_f32 v[48:49], v[38:39], v[68:69] neg_lo:[0,1] neg_hi:[0,1]
	v_pk_add_f32 v[38:39], v[56:57], v[54:55]
	v_pk_add_f32 v[54:55], v[54:55], v[56:57] neg_lo:[0,1] neg_hi:[0,1]
	v_pk_add_f32 v[62:63], v[74:75], v[86:87] neg_lo:[0,1] neg_hi:[0,1]
	v_pk_mul_f32 v[56:57], v[10:11], v[54:55] op_sel:[0,1] op_sel_hi:[0,0] neg_lo:[1,1] neg_hi:[1,0]
	v_xor_b32_e32 v69, 0x80000000, v62
	v_mov_b32_e32 v68, v63
	v_pk_add_f32 v[62:63], v[78:79], v[66:67]
	v_pk_add_f32 v[66:67], v[78:79], v[66:67] neg_lo:[0,1] neg_hi:[0,1]
	v_pk_fma_f32 v[56:57], v[10:11], v[54:55], v[56:57] op_sel_hi:[0,1,1]
	v_pk_add_f32 v[54:55], v[74:75], v[86:87]
	v_pk_mul_f32 v[74:75], v[10:11], v[66:67] op_sel:[0,1] op_sel_hi:[0,0] neg_lo:[1,1] neg_hi:[1,0]
	v_pk_fma_f32 v[66:67], v[10:11], v[66:67], v[74:75] op_sel_hi:[0,1,1] neg_lo:[1,0,0] neg_hi:[1,0,0]
	v_pk_add_f32 v[74:75], v[32:33], v[54:55]
	v_pk_add_f32 v[32:33], v[32:33], v[54:55] neg_lo:[0,1] neg_hi:[0,1]
	v_pk_add_f32 v[54:55], v[38:39], v[62:63]
	v_pk_add_f32 v[38:39], v[38:39], v[62:63] neg_lo:[0,1] neg_hi:[0,1]
	v_pk_add_f32 v[78:79], v[74:75], v[54:55]
	v_pk_add_f32 v[54:55], v[74:75], v[54:55] neg_lo:[0,1] neg_hi:[0,1]
	v_pk_add_f32 v[74:75], v[32:33], v[38:39] op_sel:[0,1] op_sel_hi:[1,0] neg_hi:[0,1]
	v_pk_add_f32 v[38:39], v[32:33], v[38:39] op_sel:[0,1] op_sel_hi:[1,0] neg_lo:[0,1]
	v_pk_add_f32 v[32:33], v[48:49], v[68:69]
	v_pk_add_f32 v[62:63], v[48:49], v[68:69] neg_lo:[0,1] neg_hi:[0,1]
	v_pk_add_f32 v[48:49], v[56:57], v[66:67]
	v_pk_add_f32 v[56:57], v[56:57], v[66:67] neg_lo:[0,1] neg_hi:[0,1]
	v_xor_b32_e32 v67, 0x80000000, v56
	v_mov_b32_e32 v66, v57
	v_pk_add_f32 v[56:57], v[32:33], v[48:49]
	v_pk_add_f32 v[48:49], v[32:33], v[48:49] neg_lo:[0,1] neg_hi:[0,1]
	v_pk_add_f32 v[68:69], v[62:63], v[66:67]
	v_pk_add_f32 v[32:33], v[62:63], v[66:67] neg_lo:[0,1] neg_hi:[0,1]
	v_pk_add_f32 v[66:67], v[64:65], v[52:53]
	v_pk_add_f32 v[52:53], v[52:53], v[64:65] neg_lo:[0,1] neg_hi:[0,1]
	v_pk_add_f32 v[62:63], v[58:59], v[80:81]
	v_pk_mul_f32 v[64:65], v[10:11], v[52:53] op_sel:[0,1] op_sel_hi:[0,0] neg_lo:[1,1] neg_hi:[1,0]
	v_pk_fma_f32 v[52:53], v[10:11], v[52:53], v[64:65] op_sel_hi:[0,1,1]
	v_pk_add_f32 v[64:65], v[72:73], v[60:61]
	v_pk_add_f32 v[60:61], v[72:73], v[60:61] neg_lo:[0,1] neg_hi:[0,1]
	v_pk_add_f32 v[58:59], v[58:59], v[80:81] neg_lo:[0,1] neg_hi:[0,1]
	v_xor_b32_e32 v73, 0x80000000, v60
	v_mov_b32_e32 v72, v61
	v_pk_add_f32 v[60:61], v[42:43], v[36:37]
	v_pk_add_f32 v[36:37], v[42:43], v[36:37] neg_lo:[0,1] neg_hi:[0,1]
	v_pk_mul_f32 v[42:43], v[10:11], v[36:37] op_sel:[0,1] op_sel_hi:[0,0] neg_lo:[1,1] neg_hi:[1,0]
	v_pk_fma_f32 v[36:37], v[10:11], v[36:37], v[42:43] op_sel_hi:[0,1,1] neg_lo:[1,0,0] neg_hi:[1,0,0]
	v_pk_add_f32 v[42:43], v[62:63], v[64:65]
	v_pk_add_f32 v[62:63], v[62:63], v[64:65] neg_lo:[0,1] neg_hi:[0,1]
	v_pk_add_f32 v[64:65], v[66:67], v[60:61]
	v_pk_add_f32 v[60:61], v[66:67], v[60:61] neg_lo:[0,1] neg_hi:[0,1]
	v_lshl_add_u32 v10, v13, 3, 0
	v_xor_b32_e32 v67, 0x80000000, v60
	v_mov_b32_e32 v66, v61
	v_pk_add_f32 v[60:61], v[42:43], v[64:65]
	v_pk_add_f32 v[64:65], v[42:43], v[64:65] neg_lo:[0,1] neg_hi:[0,1]
	v_pk_add_f32 v[80:81], v[62:63], v[66:67]
	v_pk_add_f32 v[42:43], v[62:63], v[66:67] neg_lo:[0,1] neg_hi:[0,1]
	v_pk_add_f32 v[66:67], v[52:53], v[36:37]
	v_pk_add_f32 v[36:37], v[52:53], v[36:37] neg_lo:[0,1] neg_hi:[0,1]
	v_pk_add_f32 v[62:63], v[58:59], v[72:73]
	v_pk_add_f32 v[58:59], v[58:59], v[72:73] neg_lo:[0,1] neg_hi:[0,1]
	v_pk_add_f32 v[86:87], v[62:63], v[66:67]
	v_pk_add_f32 v[52:53], v[62:63], v[66:67] neg_lo:[0,1] neg_hi:[0,1]
	v_pk_add_f32 v[62:63], v[58:59], v[36:37] op_sel:[0,1] op_sel_hi:[1,0] neg_hi:[0,1]
	v_pk_add_f32 v[36:37], v[58:59], v[36:37] op_sel:[0,1] op_sel_hi:[1,0] neg_lo:[0,1]
	v_pk_mul_f32 v[58:59], v[84:85], s[14:15] op_sel:[1,0] neg_lo:[1,0]
	v_pk_fma_f32 v[58:59], v[84:85], s[94:95], v[58:59] op_sel_hi:[0,1,1]
	ds_write_b64 v10, v[58:59]
	v_pk_fma_f32 v[58:59], v[178:179], s[90:91], v[178:179] op_sel:[1,0,0] op_sel_hi:[0,1,1]
	v_pk_mul_f32 v[66:67], v[58:59], v[78:79] op_sel:[1,1] op_sel_hi:[0,1] neg_lo:[0,1]
	v_pk_fma_f32 v[66:67], v[58:59], v[78:79], v[66:67] op_sel_hi:[1,0,1]
	ds_write_b64 v10, v[66:67] offset:4224
	v_pk_mul_f32 v[66:67], v[178:179], v[58:59] op_sel:[1,1] op_sel_hi:[0,1] neg_lo:[0,1]
	v_pk_fma_f32 v[58:59], v[178:179], v[58:59], v[66:67] op_sel_hi:[1,0,1]
	v_pk_mul_f32 v[66:67], v[58:59], v[82:83] op_sel:[1,1] op_sel_hi:[0,1] neg_lo:[0,1]
	v_pk_fma_f32 v[66:67], v[58:59], v[82:83], v[66:67] op_sel_hi:[1,0,1]
	ds_write_b64 v10, v[66:67] offset:8448
	v_pk_mul_f32 v[66:67], v[178:179], v[58:59] op_sel:[1,1] op_sel_hi:[0,1] neg_lo:[0,1]
	v_pk_fma_f32 v[58:59], v[178:179], v[58:59], v[66:67] op_sel_hi:[1,0,1]
	v_pk_mul_f32 v[66:67], v[58:59], v[60:61] op_sel:[1,1] op_sel_hi:[0,1] neg_lo:[0,1]
	v_pk_fma_f32 v[60:61], v[58:59], v[60:61], v[66:67] op_sel_hi:[1,0,1]
	ds_write_b64 v10, v[60:61] offset:12672
	v_pk_mul_f32 v[60:61], v[178:179], v[58:59] op_sel:[1,1] op_sel_hi:[0,1] neg_lo:[0,1]
	v_pk_fma_f32 v[58:59], v[178:179], v[58:59], v[60:61] op_sel_hi:[1,0,1]
	v_pk_mul_f32 v[60:61], v[70:71], v[58:59] op_sel:[1,1] op_sel_hi:[1,0] neg_lo:[1,0]
	v_pk_fma_f32 v[60:61], v[70:71], v[58:59], v[60:61] op_sel_hi:[0,1,1]
	ds_write_b64 v10, v[60:61] offset:16896
	v_pk_mul_f32 v[60:61], v[178:179], v[58:59] op_sel:[1,1] op_sel_hi:[0,1] neg_lo:[0,1]
	v_pk_fma_f32 v[58:59], v[178:179], v[58:59], v[60:61] op_sel_hi:[1,0,1]
	v_pk_mul_f32 v[60:61], v[58:59], v[56:57] op_sel:[1,1] op_sel_hi:[0,1] neg_lo:[0,1]
	v_pk_fma_f32 v[56:57], v[58:59], v[56:57], v[60:61] op_sel_hi:[1,0,1]
	ds_write_b64 v10, v[56:57] offset:21120
	v_pk_mul_f32 v[56:57], v[178:179], v[58:59] op_sel:[1,1] op_sel_hi:[0,1] neg_lo:[0,1]
	v_pk_fma_f32 v[56:57], v[178:179], v[58:59], v[56:57] op_sel_hi:[1,0,1]
	v_pk_mul_f32 v[58:59], v[76:77], v[56:57] op_sel:[1,1] op_sel_hi:[1,0] neg_lo:[1,0]
	v_pk_fma_f32 v[58:59], v[76:77], v[56:57], v[58:59] op_sel_hi:[0,1,1]
	ds_write_b64 v10, v[58:59] offset:25344
	v_pk_mul_f32 v[58:59], v[178:179], v[56:57] op_sel:[1,1] op_sel_hi:[0,1] neg_lo:[0,1]
	v_pk_fma_f32 v[56:57], v[178:179], v[56:57], v[58:59] op_sel_hi:[1,0,1]
	v_pk_mul_f32 v[58:59], v[86:87], v[56:57] op_sel:[1,1] op_sel_hi:[1,0] neg_lo:[1,0]
	v_pk_fma_f32 v[58:59], v[86:87], v[56:57], v[58:59] op_sel_hi:[0,1,1]
	ds_write_b64 v10, v[58:59] offset:29568
	v_pk_mul_f32 v[58:59], v[178:179], v[56:57] op_sel:[1,1] op_sel_hi:[0,1] neg_lo:[0,1]
	v_pk_fma_f32 v[56:57], v[178:179], v[56:57], v[58:59] op_sel_hi:[1,0,1]
	v_pk_mul_f32 v[58:59], v[46:47], v[56:57] op_sel:[1,1] op_sel_hi:[1,0] neg_lo:[1,0]
	v_pk_fma_f32 v[46:47], v[46:47], v[56:57], v[58:59] op_sel_hi:[0,1,1]
	ds_write_b64 v10, v[46:47] offset:33792
	v_pk_mul_f32 v[46:47], v[178:179], v[56:57] op_sel:[1,1] op_sel_hi:[0,1] neg_lo:[0,1]
	v_pk_fma_f32 v[46:47], v[178:179], v[56:57], v[46:47] op_sel_hi:[1,0,1]
	v_pk_mul_f32 v[56:57], v[74:75], v[46:47] op_sel:[1,1] op_sel_hi:[1,0] neg_lo:[1,0]
	v_pk_fma_f32 v[56:57], v[74:75], v[46:47], v[56:57] op_sel_hi:[0,1,1]
	ds_write_b64 v10, v[56:57] offset:38016
	v_pk_mul_f32 v[56:57], v[178:179], v[46:47] op_sel:[1,1] op_sel_hi:[0,1] neg_lo:[0,1]
	v_pk_fma_f32 v[46:47], v[178:179], v[46:47], v[56:57] op_sel_hi:[1,0,1]
	v_pk_mul_f32 v[56:57], v[50:51], v[46:47] op_sel:[1,1] op_sel_hi:[1,0] neg_lo:[1,0]
	v_pk_fma_f32 v[50:51], v[50:51], v[46:47], v[56:57] op_sel_hi:[0,1,1]
	ds_write_b64 v10, v[50:51] offset:42240
	v_pk_mul_f32 v[50:51], v[178:179], v[46:47] op_sel:[1,1] op_sel_hi:[0,1] neg_lo:[0,1]
	v_pk_fma_f32 v[46:47], v[178:179], v[46:47], v[50:51] op_sel_hi:[1,0,1]
	v_pk_mul_f32 v[50:51], v[80:81], v[46:47] op_sel:[1,1] op_sel_hi:[1,0] neg_lo:[1,0]
	v_pk_fma_f32 v[50:51], v[80:81], v[46:47], v[50:51] op_sel_hi:[0,1,1]
	ds_write_b64 v10, v[50:51] offset:46464
	v_pk_mul_f32 v[50:51], v[178:179], v[46:47] op_sel:[1,1] op_sel_hi:[0,1] neg_lo:[0,1]
	v_pk_fma_f32 v[46:47], v[178:179], v[46:47], v[50:51] op_sel_hi:[1,0,1]
	v_pk_mul_f32 v[50:51], v[40:41], v[46:47] op_sel:[1,1] op_sel_hi:[1,0] neg_lo:[1,0]
	v_pk_fma_f32 v[40:41], v[40:41], v[46:47], v[50:51] op_sel_hi:[0,1,1]
	ds_write_b64 v10, v[40:41] offset:50688
	v_pk_mul_f32 v[40:41], v[178:179], v[46:47] op_sel:[1,1] op_sel_hi:[0,1] neg_lo:[0,1]
	v_pk_fma_f32 v[40:41], v[178:179], v[46:47], v[40:41] op_sel_hi:[1,0,1]
	v_pk_mul_f32 v[46:47], v[68:69], v[40:41] op_sel:[1,1] op_sel_hi:[1,0] neg_lo:[1,0]
	v_pk_fma_f32 v[46:47], v[68:69], v[40:41], v[46:47] op_sel_hi:[0,1,1]
	ds_write_b64 v10, v[46:47] offset:54912
	v_pk_mul_f32 v[46:47], v[178:179], v[40:41] op_sel:[1,1] op_sel_hi:[0,1] neg_lo:[0,1]
	v_pk_fma_f32 v[40:41], v[178:179], v[40:41], v[46:47] op_sel_hi:[1,0,1]
	v_pk_mul_f32 v[46:47], v[44:45], v[40:41] op_sel:[1,1] op_sel_hi:[1,0] neg_lo:[1,0]
	v_pk_fma_f32 v[44:45], v[44:45], v[40:41], v[46:47] op_sel_hi:[0,1,1]
	ds_write_b64 v10, v[44:45] offset:59136
	v_pk_mul_f32 v[44:45], v[178:179], v[40:41] op_sel:[1,1] op_sel_hi:[0,1] neg_lo:[0,1]
	v_pk_fma_f32 v[40:41], v[178:179], v[40:41], v[44:45] op_sel_hi:[1,0,1]
	v_pk_mul_f32 v[44:45], v[62:63], v[40:41] op_sel:[1,1] op_sel_hi:[1,0] neg_lo:[1,0]
	v_pk_fma_f32 v[44:45], v[62:63], v[40:41], v[44:45] op_sel_hi:[0,1,1]
	ds_write_b64 v10, v[44:45] offset:63360
	v_pk_mul_f32 v[44:45], v[178:179], v[40:41] op_sel:[1,1] op_sel_hi:[0,1] neg_lo:[0,1]
	v_pk_fma_f32 v[40:41], v[178:179], v[40:41], v[44:45] op_sel_hi:[1,0,1]
	v_pk_mul_f32 v[44:45], v[30:31], v[40:41] op_sel:[1,1] op_sel_hi:[1,0] neg_lo:[1,0]
	v_add_u32_e32 v13, 0x10800, v10
	v_pk_fma_f32 v[30:31], v[30:31], v[40:41], v[44:45] op_sel_hi:[0,1,1]
	ds_write_b64 v13, v[30:31]
	v_pk_mul_f32 v[30:31], v[178:179], v[40:41] op_sel:[1,1] op_sel_hi:[0,1] neg_lo:[0,1]
	v_pk_fma_f32 v[30:31], v[178:179], v[40:41], v[30:31] op_sel_hi:[1,0,1]
	v_pk_mul_f32 v[40:41], v[54:55], v[30:31] op_sel:[1,1] op_sel_hi:[1,0] neg_lo:[1,0]
	v_add_u32_e32 v13, 0x11880, v10
	v_pk_fma_f32 v[40:41], v[54:55], v[30:31], v[40:41] op_sel_hi:[0,1,1]
	ds_write_b64 v13, v[40:41]
	v_pk_mul_f32 v[40:41], v[178:179], v[30:31] op_sel:[1,1] op_sel_hi:[0,1] neg_lo:[0,1]
	v_pk_fma_f32 v[30:31], v[178:179], v[30:31], v[40:41] op_sel_hi:[1,0,1]
	v_pk_mul_f32 v[40:41], v[34:35], v[30:31] op_sel:[1,1] op_sel_hi:[1,0] neg_lo:[1,0]
	v_add_u32_e32 v13, 0x12900, v10
	v_pk_fma_f32 v[34:35], v[34:35], v[30:31], v[40:41] op_sel_hi:[0,1,1]
	ds_write_b64 v13, v[34:35]
	v_pk_mul_f32 v[34:35], v[178:179], v[30:31] op_sel:[1,1] op_sel_hi:[0,1] neg_lo:[0,1]
	v_pk_fma_f32 v[30:31], v[178:179], v[30:31], v[34:35] op_sel_hi:[1,0,1]
	v_pk_mul_f32 v[34:35], v[64:65], v[30:31] op_sel:[1,1] op_sel_hi:[1,0] neg_lo:[1,0]
	v_add_u32_e32 v13, 0x13980, v10
	v_pk_fma_f32 v[34:35], v[64:65], v[30:31], v[34:35] op_sel_hi:[0,1,1]
	ds_write_b64 v13, v[34:35]
	v_pk_mul_f32 v[34:35], v[178:179], v[30:31] op_sel:[1,1] op_sel_hi:[0,1] neg_lo:[0,1]
	v_pk_fma_f32 v[30:31], v[178:179], v[30:31], v[34:35] op_sel_hi:[1,0,1]
	v_pk_mul_f32 v[34:35], v[26:27], v[30:31] op_sel:[1,1] op_sel_hi:[1,0] neg_lo:[1,0]
	v_add_u32_e32 v13, 0x14a00, v10
	v_pk_fma_f32 v[26:27], v[26:27], v[30:31], v[34:35] op_sel_hi:[0,1,1]
	ds_write_b64 v13, v[26:27]
	v_pk_mul_f32 v[26:27], v[178:179], v[30:31] op_sel:[1,1] op_sel_hi:[0,1] neg_lo:[0,1]
	v_pk_fma_f32 v[26:27], v[178:179], v[30:31], v[26:27] op_sel_hi:[1,0,1]
	v_pk_mul_f32 v[30:31], v[48:49], v[26:27] op_sel:[1,1] op_sel_hi:[1,0] neg_lo:[1,0]
	v_add_u32_e32 v13, 0x15a80, v10
	v_pk_fma_f32 v[30:31], v[48:49], v[26:27], v[30:31] op_sel_hi:[0,1,1]
	ds_write_b64 v13, v[30:31]
	v_pk_mul_f32 v[30:31], v[178:179], v[26:27] op_sel:[1,1] op_sel_hi:[0,1] neg_lo:[0,1]
	v_pk_fma_f32 v[26:27], v[178:179], v[26:27], v[30:31] op_sel_hi:[1,0,1]
	v_pk_mul_f32 v[30:31], v[28:29], v[26:27] op_sel:[1,1] op_sel_hi:[1,0] neg_lo:[1,0]
	v_add_u32_e32 v13, 0x16b00, v10
	v_pk_fma_f32 v[28:29], v[28:29], v[26:27], v[30:31] op_sel_hi:[0,1,1]
	ds_write_b64 v13, v[28:29]
	v_pk_mul_f32 v[28:29], v[178:179], v[26:27] op_sel:[1,1] op_sel_hi:[0,1] neg_lo:[0,1]
	v_pk_fma_f32 v[26:27], v[178:179], v[26:27], v[28:29] op_sel_hi:[1,0,1]
	v_pk_mul_f32 v[28:29], v[52:53], v[26:27] op_sel:[1,1] op_sel_hi:[1,0] neg_lo:[1,0]
	v_add_u32_e32 v13, 0x17b80, v10
	v_pk_fma_f32 v[28:29], v[52:53], v[26:27], v[28:29] op_sel_hi:[0,1,1]
	ds_write_b64 v13, v[28:29]
	v_pk_mul_f32 v[28:29], v[178:179], v[26:27] op_sel:[1,1] op_sel_hi:[0,1] neg_lo:[0,1]
	v_pk_fma_f32 v[26:27], v[178:179], v[26:27], v[28:29] op_sel_hi:[1,0,1]
	v_pk_mul_f32 v[28:29], v[22:23], v[26:27] op_sel:[1,1] op_sel_hi:[1,0] neg_lo:[1,0]
	v_add_u32_e32 v13, 0x18c00, v10
	v_pk_fma_f32 v[22:23], v[22:23], v[26:27], v[28:29] op_sel_hi:[0,1,1]
	ds_write_b64 v13, v[22:23]
	v_pk_mul_f32 v[22:23], v[178:179], v[26:27] op_sel:[1,1] op_sel_hi:[0,1] neg_lo:[0,1]
	v_pk_fma_f32 v[22:23], v[178:179], v[26:27], v[22:23] op_sel_hi:[1,0,1]
	v_pk_mul_f32 v[26:27], v[38:39], v[22:23] op_sel:[1,1] op_sel_hi:[1,0] neg_lo:[1,0]
	v_add_u32_e32 v13, 0x19c80, v10
	v_pk_fma_f32 v[26:27], v[38:39], v[22:23], v[26:27] op_sel_hi:[0,1,1]
	ds_write_b64 v13, v[26:27]
	v_pk_mul_f32 v[26:27], v[178:179], v[22:23] op_sel:[1,1] op_sel_hi:[0,1] neg_lo:[0,1]
	v_pk_fma_f32 v[22:23], v[178:179], v[22:23], v[26:27] op_sel_hi:[1,0,1]
	v_pk_mul_f32 v[26:27], v[24:25], v[22:23] op_sel:[1,1] op_sel_hi:[1,0] neg_lo:[1,0]
	v_add_u32_e32 v13, 0x1ad00, v10
	v_pk_fma_f32 v[24:25], v[24:25], v[22:23], v[26:27] op_sel_hi:[0,1,1]
	ds_write_b64 v13, v[24:25]
	v_pk_mul_f32 v[24:25], v[178:179], v[22:23] op_sel:[1,1] op_sel_hi:[0,1] neg_lo:[0,1]
	v_pk_fma_f32 v[22:23], v[178:179], v[22:23], v[24:25] op_sel_hi:[1,0,1]
	v_pk_mul_f32 v[24:25], v[42:43], v[22:23] op_sel:[1,1] op_sel_hi:[1,0] neg_lo:[1,0]
	v_add_u32_e32 v13, 0x1bd80, v10
	v_pk_fma_f32 v[24:25], v[42:43], v[22:23], v[24:25] op_sel_hi:[0,1,1]
	ds_write_b64 v13, v[24:25]
	v_pk_mul_f32 v[24:25], v[178:179], v[22:23] op_sel:[1,1] op_sel_hi:[0,1] neg_lo:[0,1]
	v_pk_fma_f32 v[22:23], v[178:179], v[22:23], v[24:25] op_sel_hi:[1,0,1]
	v_pk_mul_f32 v[24:25], v[18:19], v[22:23] op_sel:[1,1] op_sel_hi:[1,0] neg_lo:[1,0]
	v_add_u32_e32 v13, 0x1ce00, v10
	v_pk_fma_f32 v[18:19], v[18:19], v[22:23], v[24:25] op_sel_hi:[0,1,1]
	ds_write_b64 v13, v[18:19]
	v_pk_mul_f32 v[18:19], v[178:179], v[22:23] op_sel:[1,1] op_sel_hi:[0,1] neg_lo:[0,1]
	v_pk_fma_f32 v[18:19], v[178:179], v[22:23], v[18:19] op_sel_hi:[1,0,1]
	v_pk_mul_f32 v[22:23], v[32:33], v[18:19] op_sel:[1,1] op_sel_hi:[1,0] neg_lo:[1,0]
	v_add_u32_e32 v13, 0x1de80, v10
	v_pk_fma_f32 v[22:23], v[32:33], v[18:19], v[22:23] op_sel_hi:[0,1,1]
	ds_write_b64 v13, v[22:23]
	v_pk_mul_f32 v[22:23], v[178:179], v[18:19] op_sel:[1,1] op_sel_hi:[0,1] neg_lo:[0,1]
	v_pk_fma_f32 v[18:19], v[178:179], v[18:19], v[22:23] op_sel_hi:[1,0,1]
	v_pk_mul_f32 v[22:23], v[20:21], v[18:19] op_sel:[1,1] op_sel_hi:[1,0] neg_lo:[1,0]
	v_add_u32_e32 v13, 0x1ef00, v10
	v_pk_fma_f32 v[20:21], v[20:21], v[18:19], v[22:23] op_sel_hi:[0,1,1]
	ds_write_b64 v13, v[20:21]
	v_pk_mul_f32 v[20:21], v[178:179], v[18:19] op_sel:[1,1] op_sel_hi:[0,1] neg_lo:[0,1]
	v_pk_fma_f32 v[16:17], v[178:179], v[18:19], v[20:21] op_sel_hi:[1,0,1]
	v_pk_mul_f32 v[18:19], v[36:37], v[16:17] op_sel:[1,1] op_sel_hi:[1,0] neg_lo:[1,0]
	v_add_u32_e32 v10, 0x1ff80, v10
	v_pk_fma_f32 v[16:17], v[36:37], v[16:17], v[18:19] op_sel_hi:[0,1,1]
	ds_write_b64 v10, v[16:17]
	v_mov_b32_e32 v10, v174
	v_mov_b32_e32 v13, v172
	s_waitcnt lgkmcnt(0)
	s_barrier
	v_mov_b32_e32 v16, v180
	v_add_u32_e32 v15, v13, v10
	v_lshl_add_u32 v75, v15, 3, 0
	v_xad_u32 v15, v13, 1, v10
	v_lshl_add_u32 v74, v15, 3, 0
	v_xad_u32 v15, v13, 2, v10
	v_lshl_add_u32 v73, v15, 3, 0
	v_xad_u32 v15, v13, 3, v10
	v_lshl_add_u32 v72, v15, 3, 0
	v_xad_u32 v15, v13, 4, v10
	v_lshl_add_u32 v71, v15, 3, 0
	v_xad_u32 v15, v13, 5, v10
	v_lshl_add_u32 v70, v15, 3, 0
	v_xad_u32 v15, v13, 6, v10
	v_lshl_add_u32 v69, v15, 3, 0
	v_xad_u32 v15, v13, 7, v10
	v_lshl_add_u32 v68, v15, 3, 0
	v_xad_u32 v15, v13, 8, v10
	v_lshl_add_u32 v15, v15, 3, 0
	v_add_u32_e32 v67, 0x800, v15
	v_xad_u32 v15, v13, 9, v10
	v_lshl_add_u32 v15, v15, 3, 0
	v_add_u32_e32 v66, 0x800, v15
	v_xad_u32 v15, v13, 10, v10
	v_lshl_add_u32 v15, v15, 3, 0
	v_add_u32_e32 v65, 0x800, v15
	v_xad_u32 v15, v13, 11, v10
	v_lshl_add_u32 v15, v15, 3, 0
	v_add_u32_e32 v64, 0x800, v15
	v_xad_u32 v15, v13, 12, v10
	v_mov_b32_e32 v17, v181
	v_lshl_add_u32 v15, v15, 3, 0
	ds_read2_b64 v[18:21], v75 offset1:16
	ds_read2_b64 v[40:43], v67 offset1:16
	v_add_u32_e32 v63, 0x800, v15
	v_xad_u32 v15, v13, 13, v10
	v_lshl_add_u32 v15, v15, 3, 0
	v_add_u32_e32 v62, 0x800, v15
	v_xad_u32 v15, v13, 14, v10
	v_xad_u32 v10, v13, 15, v10
	ds_read2_b64 v[22:25], v74 offset0:32 offset1:48
	ds_read2_b64 v[48:51], v66 offset0:32 offset1:48
	v_lshl_add_u32 v15, v15, 3, 0
	v_lshl_add_u32 v10, v10, 3, 0
	v_add_u32_e32 v15, 0x800, v15
	v_add_u32_e32 v13, 0x800, v10
	v_mov_b32_e32 v10, v1
	ds_read2_b64 v[26:29], v73 offset0:64 offset1:80
	ds_read2_b64 v[58:61], v72 offset0:96 offset1:112
	ds_read2_b64 v[76:79], v71 offset0:128 offset1:144
	ds_read2_b64 v[80:83], v70 offset0:160 offset1:176
	ds_read2_b64 v[84:87], v69 offset0:192 offset1:208
	ds_read2_b64 v[88:91], v68 offset0:224 offset1:240
	ds_read2_b64 v[54:57], v65 offset0:64 offset1:80
	ds_read2_b64 v[92:95], v64 offset0:96 offset1:112
	ds_read2_b64 v[96:99], v63 offset0:128 offset1:144
	ds_read2_b64 v[100:103], v62 offset0:160 offset1:176
	ds_read2_b64 v[104:107], v15 offset0:192 offset1:208
	ds_read2_b64 v[108:111], v13 offset0:224 offset1:240
	s_waitcnt lgkmcnt(14)
	v_pk_add_f32 v[112:113], v[18:19], v[40:41]
	v_pk_add_f32 v[40:41], v[18:19], v[40:41] neg_lo:[0,1] neg_hi:[0,1]
	v_pk_add_f32 v[18:19], v[20:21], v[42:43]
	v_pk_add_f32 v[20:21], v[20:21], v[42:43] neg_lo:[0,1] neg_hi:[0,1]
	v_mov_b32_e32 v30, v164
	v_mov_b32_e32 v32, v165
	v_mov_b32_e32 v34, v166
	v_mov_b32_e32 v10, v167
	v_mov_b32_e32 v38, v168
	v_mov_b32_e32 v36, v169
	v_mov_b32_e32 v46, v170
	v_mov_b32_e32 v31, v171
	v_pk_mul_f32 v[42:43], v[20:21], v[46:47] op_sel:[1,0] op_sel_hi:[0,0] neg_lo:[1,1] neg_hi:[0,1]
	v_pk_fma_f32 v[44:45], v[20:21], v[30:31], v[42:43] op_sel_hi:[1,0,1]
	s_waitcnt lgkmcnt(12)
	v_pk_add_f32 v[20:21], v[22:23], v[48:49]
	v_pk_add_f32 v[22:23], v[22:23], v[48:49] neg_lo:[0,1] neg_hi:[0,1]
	v_pk_mul_f32 v[42:43], v[22:23], v[36:37] op_sel:[1,0] op_sel_hi:[0,0] neg_lo:[1,1] neg_hi:[0,1]
	v_pk_fma_f32 v[48:49], v[22:23], v[32:33], v[42:43] op_sel_hi:[1,0,1]
	v_pk_add_f32 v[22:23], v[24:25], v[50:51]
	v_pk_add_f32 v[24:25], v[24:25], v[50:51] neg_lo:[0,1] neg_hi:[0,1]
	v_pk_mul_f32 v[42:43], v[24:25], v[38:39] op_sel:[1,0] op_sel_hi:[0,0] neg_lo:[1,1] neg_hi:[0,1]
	v_pk_fma_f32 v[52:53], v[24:25], v[34:35], v[42:43] op_sel_hi:[1,0,1]
	s_waitcnt lgkmcnt(5)
	v_pk_add_f32 v[24:25], v[26:27], v[54:55]
	v_pk_add_f32 v[26:27], v[26:27], v[54:55] neg_lo:[0,1] neg_hi:[0,1]
	v_pk_mul_f32 v[42:43], v[26:27], v[10:11] op_sel:[1,0] op_sel_hi:[0,0] neg_lo:[1,1] neg_hi:[0,1]
	v_pk_fma_f32 v[54:55], v[26:27], v[10:11], v[42:43] op_sel_hi:[1,0,1]
	v_pk_add_f32 v[26:27], v[28:29], v[56:57]
	v_pk_add_f32 v[28:29], v[28:29], v[56:57] neg_lo:[0,1] neg_hi:[0,1]
	v_pk_mul_f32 v[42:43], v[28:29], v[38:39] op_sel_hi:[1,0]
	v_pk_fma_f32 v[56:57], v[28:29], v[34:35], v[42:43] op_sel:[1,0,0] op_sel_hi:[0,0,1] neg_lo:[1,1,0] neg_hi:[0,1,0]
	s_waitcnt lgkmcnt(4)
	v_pk_add_f32 v[42:43], v[58:59], v[92:93] neg_lo:[0,1] neg_hi:[0,1]
	v_pk_add_f32 v[28:29], v[58:59], v[92:93]
	v_pk_mul_f32 v[50:51], v[42:43], v[36:37] op_sel_hi:[1,0]
	v_pk_fma_f32 v[58:59], v[42:43], v[32:33], v[50:51] op_sel:[1,0,0] op_sel_hi:[0,0,1] neg_lo:[1,1,0] neg_hi:[0,1,0]
	v_pk_add_f32 v[50:51], v[60:61], v[94:95] neg_lo:[0,1] neg_hi:[0,1]
	v_pk_add_f32 v[42:43], v[60:61], v[94:95]
	v_pk_mul_f32 v[60:61], v[50:51], v[46:47] op_sel_hi:[1,0]
	v_xor_b32_e32 v92, 0x80000000, v51
	v_mov_b32_e32 v93, v50
	s_waitcnt lgkmcnt(3)
	v_pk_add_f32 v[50:51], v[76:77], v[96:97]
	v_pk_add_f32 v[76:77], v[76:77], v[96:97] neg_lo:[0,1] neg_hi:[0,1]
	v_pk_fma_f32 v[60:61], v[92:93], v[30:31], v[60:61] op_sel_hi:[1,0,1] neg_lo:[0,1,0] neg_hi:[0,1,0]
	v_xor_b32_e32 v93, 0x80000000, v76
	v_mov_b32_e32 v92, v77
	v_pk_add_f32 v[76:77], v[78:79], v[98:99]
	v_pk_add_f32 v[78:79], v[78:79], v[98:99] neg_lo:[0,1] neg_hi:[0,1]
	v_pk_mul_f32 v[94:95], v[78:79], v[46:47] op_sel_hi:[1,0] neg_lo:[0,1] neg_hi:[0,1]
	v_pk_fma_f32 v[78:79], v[78:79], v[30:31], v[94:95] op_sel:[1,0,0] op_sel_hi:[0,0,1] neg_lo:[1,1,0] neg_hi:[0,1,0]
	s_waitcnt lgkmcnt(2)
	v_pk_add_f32 v[94:95], v[80:81], v[100:101]
	v_pk_add_f32 v[80:81], v[80:81], v[100:101] neg_lo:[0,1] neg_hi:[0,1]
	v_pk_mul_f32 v[96:97], v[80:81], v[36:37] op_sel_hi:[1,0] neg_lo:[0,1] neg_hi:[0,1]
	v_pk_fma_f32 v[80:81], v[80:81], v[32:33], v[96:97] op_sel:[1,0,0] op_sel_hi:[0,0,1] neg_lo:[1,1,0] neg_hi:[0,1,0]
	v_pk_add_f32 v[96:97], v[82:83], v[102:103]
	v_pk_add_f32 v[82:83], v[82:83], v[102:103] neg_lo:[0,1] neg_hi:[0,1]
	v_pk_mul_f32 v[98:99], v[82:83], v[38:39] op_sel_hi:[1,0] neg_lo:[0,1] neg_hi:[0,1]
	v_pk_fma_f32 v[82:83], v[82:83], v[34:35], v[98:99] op_sel:[1,0,0] op_sel_hi:[0,0,1] neg_lo:[1,1,0] neg_hi:[0,1,0]
	s_waitcnt lgkmcnt(1)
	v_pk_add_f32 v[98:99], v[84:85], v[104:105]
	v_pk_add_f32 v[84:85], v[84:85], v[104:105] neg_lo:[0,1] neg_hi:[0,1]
	v_pk_mul_f32 v[100:101], v[84:85], v[10:11] op_sel:[1,0] op_sel_hi:[0,0] neg_lo:[1,1] neg_hi:[0,1]
	v_pk_fma_f32 v[84:85], v[84:85], v[10:11], v[100:101] op_sel_hi:[1,0,1] neg_lo:[0,1,0] neg_hi:[0,1,0]
	v_pk_add_f32 v[100:101], v[86:87], v[106:107]
	v_pk_add_f32 v[86:87], v[86:87], v[106:107] neg_lo:[0,1] neg_hi:[0,1]
	v_pk_mul_f32 v[38:39], v[86:87], v[38:39] op_sel:[1,0] op_sel_hi:[0,0] neg_lo:[1,1] neg_hi:[0,1]
	v_pk_fma_f32 v[86:87], v[86:87], v[34:35], v[38:39] op_sel_hi:[1,0,1] neg_lo:[0,1,0] neg_hi:[0,1,0]
	s_waitcnt lgkmcnt(0)
	v_pk_add_f32 v[38:39], v[88:89], v[108:109] neg_lo:[0,1] neg_hi:[0,1]
	v_pk_add_f32 v[34:35], v[88:89], v[108:109]
	v_pk_mul_f32 v[88:89], v[38:39], v[36:37] op_sel:[1,0] op_sel_hi:[0,0] neg_lo:[1,1] neg_hi:[0,1]
	v_pk_fma_f32 v[88:89], v[38:39], v[32:33], v[88:89] op_sel_hi:[1,0,1] neg_lo:[0,1,0] neg_hi:[0,1,0]
	v_pk_add_f32 v[38:39], v[90:91], v[110:111]
	v_pk_add_f32 v[90:91], v[90:91], v[110:111] neg_lo:[0,1] neg_hi:[0,1]
	v_pk_mul_f32 v[46:47], v[90:91], v[46:47] op_sel:[1,0] op_sel_hi:[0,0] neg_lo:[1,1] neg_hi:[0,1]
	v_pk_fma_f32 v[90:91], v[90:91], v[30:31], v[46:47] op_sel_hi:[1,0,1] neg_lo:[0,1,0] neg_hi:[0,1,0]
	v_pk_add_f32 v[46:47], v[18:19], v[76:77]
	v_pk_add_f32 v[18:19], v[18:19], v[76:77] neg_lo:[0,1] neg_hi:[0,1]
	v_pk_add_f32 v[30:31], v[112:113], v[50:51]
	v_pk_mul_f32 v[76:77], v[18:19], v[36:37] op_sel:[1,0] op_sel_hi:[0,0] neg_lo:[1,1] neg_hi:[0,1]
	v_pk_add_f32 v[50:51], v[112:113], v[50:51] neg_lo:[0,1] neg_hi:[0,1]
	v_pk_fma_f32 v[76:77], v[18:19], v[32:33], v[76:77] op_sel_hi:[1,0,1]
	v_pk_add_f32 v[18:19], v[20:21], v[94:95]
	v_pk_add_f32 v[20:21], v[20:21], v[94:95] neg_lo:[0,1] neg_hi:[0,1]
	v_pk_mul_f32 v[94:95], v[20:21], v[10:11] op_sel:[1,0] op_sel_hi:[0,0] neg_lo:[1,1] neg_hi:[0,1]
	v_pk_fma_f32 v[20:21], v[20:21], v[10:11], v[94:95] op_sel_hi:[1,0,1]
	v_pk_add_f32 v[94:95], v[22:23], v[96:97]
	v_pk_add_f32 v[22:23], v[22:23], v[96:97] neg_lo:[0,1] neg_hi:[0,1]
	v_pk_mul_f32 v[96:97], v[22:23], v[36:37] op_sel_hi:[1,0]
	v_xor_b32_e32 v102, 0x80000000, v23
	v_mov_b32_e32 v103, v22
	v_pk_add_f32 v[22:23], v[24:25], v[98:99]
	v_pk_add_f32 v[24:25], v[24:25], v[98:99] neg_lo:[0,1] neg_hi:[0,1]
	v_pk_fma_f32 v[96:97], v[102:103], v[32:33], v[96:97] op_sel_hi:[1,0,1] neg_lo:[0,1,0] neg_hi:[0,1,0]
	v_xor_b32_e32 v99, 0x80000000, v24
	v_mov_b32_e32 v98, v25
	v_pk_add_f32 v[24:25], v[26:27], v[100:101]
	v_pk_add_f32 v[26:27], v[26:27], v[100:101] neg_lo:[0,1] neg_hi:[0,1]
	v_pk_mul_f32 v[100:101], v[26:27], v[36:37] op_sel_hi:[1,0] neg_lo:[0,1] neg_hi:[0,1]
	v_xor_b32_e32 v102, 0x80000000, v27
	v_mov_b32_e32 v103, v26
	v_pk_add_f32 v[26:27], v[28:29], v[34:35]
	v_pk_add_f32 v[28:29], v[28:29], v[34:35] neg_lo:[0,1] neg_hi:[0,1]
	v_pk_fma_f32 v[100:101], v[102:103], v[32:33], v[100:101] op_sel_hi:[1,0,1] neg_lo:[0,1,0] neg_hi:[0,1,0]
	v_pk_mul_f32 v[34:35], v[28:29], v[10:11] op_sel:[1,0] op_sel_hi:[0,0] neg_lo:[1,1] neg_hi:[0,1]
	v_pk_add_f32 v[102:103], v[30:31], v[22:23] neg_lo:[0,1] neg_hi:[0,1]
	v_pk_fma_f32 v[28:29], v[28:29], v[10:11], v[34:35] op_sel_hi:[1,0,1] neg_lo:[0,1,0] neg_hi:[0,1,0]
	v_pk_add_f32 v[34:35], v[42:43], v[38:39]
	v_pk_add_f32 v[38:39], v[42:43], v[38:39] neg_lo:[0,1] neg_hi:[0,1]
	v_pk_mul_f32 v[42:43], v[38:39], v[36:37] op_sel:[1,0] op_sel_hi:[0,0] neg_lo:[1,1] neg_hi:[0,1]
	v_pk_fma_f32 v[42:43], v[38:39], v[32:33], v[42:43] op_sel_hi:[1,0,1] neg_lo:[0,1,0] neg_hi:[0,1,0]
	v_pk_add_f32 v[38:39], v[30:31], v[22:23]
	v_pk_add_f32 v[22:23], v[46:47], v[24:25]
	v_pk_add_f32 v[24:25], v[46:47], v[24:25] neg_lo:[0,1] neg_hi:[0,1]
	v_pk_mul_f32 v[30:31], v[24:25], v[10:11] op_sel:[1,0] op_sel_hi:[0,0] neg_lo:[1,1] neg_hi:[0,1]
	v_pk_fma_f32 v[24:25], v[24:25], v[10:11], v[30:31] op_sel_hi:[1,0,1]
	v_pk_add_f32 v[30:31], v[18:19], v[26:27]
	v_pk_add_f32 v[18:19], v[18:19], v[26:27] neg_lo:[0,1] neg_hi:[0,1]
	v_xor_b32_e32 v27, 0x80000000, v18
	v_mov_b32_e32 v26, v19
	v_pk_add_f32 v[18:19], v[94:95], v[34:35]
	v_pk_add_f32 v[34:35], v[94:95], v[34:35] neg_lo:[0,1] neg_hi:[0,1]
	v_pk_mul_f32 v[46:47], v[34:35], v[10:11] op_sel:[1,0] op_sel_hi:[0,0] neg_lo:[1,1] neg_hi:[0,1]
	v_pk_fma_f32 v[34:35], v[34:35], v[10:11], v[46:47] op_sel_hi:[1,0,1] neg_lo:[0,1,0] neg_hi:[0,1,0]
	v_pk_add_f32 v[46:47], v[38:39], v[30:31]
	v_pk_add_f32 v[38:39], v[38:39], v[30:31] neg_lo:[0,1] neg_hi:[0,1]
	v_pk_add_f32 v[30:31], v[22:23], v[18:19]
	v_pk_add_f32 v[18:19], v[22:23], v[18:19] neg_lo:[0,1] neg_hi:[0,1]
	v_pk_add_f32 v[94:95], v[46:47], v[30:31]
	v_xor_b32_e32 v23, 0x80000000, v18
	v_mov_b32_e32 v22, v19
	v_pk_add_f32 v[18:19], v[102:103], v[26:27]
	v_pk_add_f32 v[102:103], v[102:103], v[26:27] neg_lo:[0,1] neg_hi:[0,1]
	v_pk_add_f32 v[26:27], v[24:25], v[34:35]
	v_pk_add_f32 v[24:25], v[24:25], v[34:35] neg_lo:[0,1] neg_hi:[0,1]
	v_pk_add_f32 v[30:31], v[46:47], v[30:31] neg_lo:[0,1] neg_hi:[0,1]
	v_xor_b32_e32 v35, 0x80000000, v24
	v_mov_b32_e32 v34, v25
	v_pk_add_f32 v[24:25], v[50:51], v[98:99]
	v_pk_add_f32 v[98:99], v[50:51], v[98:99] neg_lo:[0,1] neg_hi:[0,1]
	v_pk_add_f32 v[50:51], v[76:77], v[100:101] neg_lo:[0,1] neg_hi:[0,1]
	v_pk_add_f32 v[46:47], v[38:39], v[22:23]
	v_pk_add_f32 v[22:23], v[38:39], v[22:23] neg_lo:[0,1] neg_hi:[0,1]
	v_pk_add_f32 v[104:105], v[18:19], v[26:27]
	v_pk_add_f32 v[26:27], v[18:19], v[26:27] neg_lo:[0,1] neg_hi:[0,1]
	v_pk_add_f32 v[38:39], v[102:103], v[34:35]
	v_pk_add_f32 v[18:19], v[102:103], v[34:35] neg_lo:[0,1] neg_hi:[0,1]
	v_pk_add_f32 v[34:35], v[76:77], v[100:101]
	v_pk_mul_f32 v[76:77], v[10:11], v[50:51] op_sel:[0,1] op_sel_hi:[0,0] neg_lo:[1,1] neg_hi:[1,0]
	v_pk_fma_f32 v[76:77], v[10:11], v[50:51], v[76:77] op_sel_hi:[0,1,1]
	v_pk_add_f32 v[50:51], v[20:21], v[28:29]
	v_pk_add_f32 v[20:21], v[20:21], v[28:29] neg_lo:[0,1] neg_hi:[0,1]
	v_xor_b32_e32 v29, 0x80000000, v20
	v_mov_b32_e32 v28, v21
	v_pk_add_f32 v[20:21], v[96:97], v[42:43]
	v_pk_add_f32 v[42:43], v[96:97], v[42:43] neg_lo:[0,1] neg_hi:[0,1]
	v_pk_mul_f32 v[96:97], v[10:11], v[42:43] op_sel:[0,1] op_sel_hi:[0,0] neg_lo:[1,1] neg_hi:[1,0]
	v_pk_fma_f32 v[42:43], v[10:11], v[42:43], v[96:97] op_sel_hi:[0,1,1] neg_lo:[1,0,0] neg_hi:[1,0,0]
	v_pk_add_f32 v[96:97], v[24:25], v[50:51]
	v_pk_add_f32 v[24:25], v[24:25], v[50:51] neg_lo:[0,1] neg_hi:[0,1]
	v_pk_add_f32 v[50:51], v[34:35], v[20:21]
	v_pk_add_f32 v[20:21], v[34:35], v[20:21] neg_lo:[0,1] neg_hi:[0,1]
	v_pk_add_f32 v[102:103], v[96:97], v[50:51]
	v_xor_b32_e32 v101, 0x80000000, v20
	v_mov_b32_e32 v100, v21
	v_pk_add_f32 v[34:35], v[96:97], v[50:51] neg_lo:[0,1] neg_hi:[0,1]
	v_pk_add_f32 v[20:21], v[98:99], v[28:29]
	v_pk_add_f32 v[96:97], v[98:99], v[28:29] neg_lo:[0,1] neg_hi:[0,1]
	v_pk_add_f32 v[28:29], v[76:77], v[42:43]
	v_pk_add_f32 v[42:43], v[76:77], v[42:43] neg_lo:[0,1] neg_hi:[0,1]
	v_pk_add_f32 v[98:99], v[20:21], v[28:29]
	v_xor_b32_e32 v77, 0x80000000, v42
	v_mov_b32_e32 v76, v43
	v_pk_add_f32 v[28:29], v[20:21], v[28:29] neg_lo:[0,1] neg_hi:[0,1]
	v_pk_add_f32 v[42:43], v[96:97], v[76:77]
	v_pk_add_f32 v[20:21], v[96:97], v[76:77] neg_lo:[0,1] neg_hi:[0,1]
	v_pk_add_f32 v[76:77], v[40:41], v[92:93]
	v_pk_add_f32 v[92:93], v[40:41], v[92:93] neg_lo:[0,1] neg_hi:[0,1]
	v_pk_add_f32 v[40:41], v[44:45], v[78:79]
	v_pk_add_f32 v[44:45], v[44:45], v[78:79] neg_lo:[0,1] neg_hi:[0,1]
	v_pk_add_f32 v[50:51], v[24:25], v[100:101]
	v_pk_mul_f32 v[78:79], v[36:37], v[44:45] op_sel:[0,1] op_sel_hi:[0,0] neg_lo:[1,1] neg_hi:[1,0]
	v_pk_fma_f32 v[44:45], v[32:33], v[44:45], v[78:79] op_sel_hi:[0,1,1]
	v_pk_add_f32 v[78:79], v[48:49], v[80:81]
	v_pk_add_f32 v[48:49], v[48:49], v[80:81] neg_lo:[0,1] neg_hi:[0,1]
	v_pk_add_f32 v[24:25], v[24:25], v[100:101] neg_lo:[0,1] neg_hi:[0,1]
	v_pk_mul_f32 v[80:81], v[10:11], v[48:49] op_sel:[0,1] op_sel_hi:[0,0] neg_lo:[1,1] neg_hi:[1,0]
	v_pk_fma_f32 v[80:81], v[10:11], v[48:49], v[80:81] op_sel_hi:[0,1,1]
	v_pk_add_f32 v[48:49], v[52:53], v[82:83]
	v_pk_add_f32 v[52:53], v[52:53], v[82:83] neg_lo:[0,1] neg_hi:[0,1]
	v_pk_mul_f32 v[82:83], v[32:33], v[52:53] op_sel:[0,1] op_sel_hi:[0,0] neg_lo:[1,1] neg_hi:[1,0]
	v_pk_fma_f32 v[52:53], v[36:37], v[52:53], v[82:83] op_sel_hi:[0,1,1]
	v_pk_add_f32 v[82:83], v[54:55], v[84:85]
	v_pk_add_f32 v[54:55], v[54:55], v[84:85] neg_lo:[0,1] neg_hi:[0,1]
	v_xor_b32_e32 v85, 0x80000000, v54
	v_mov_b32_e32 v84, v55
	v_pk_add_f32 v[54:55], v[56:57], v[86:87]
	v_pk_add_f32 v[56:57], v[56:57], v[86:87] neg_lo:[0,1] neg_hi:[0,1]
	v_pk_mul_f32 v[86:87], v[32:33], v[56:57] op_sel:[0,1] op_sel_hi:[0,0] neg_lo:[1,1] neg_hi:[1,0]
	v_pk_fma_f32 v[56:57], v[36:37], v[56:57], v[86:87] op_sel_hi:[0,1,1] neg_lo:[1,0,0] neg_hi:[1,0,0]
	v_pk_add_f32 v[86:87], v[58:59], v[88:89]
	v_pk_add_f32 v[58:59], v[58:59], v[88:89] neg_lo:[0,1] neg_hi:[0,1]
	v_pk_mul_f32 v[88:89], v[10:11], v[58:59] op_sel:[0,1] op_sel_hi:[0,0] neg_lo:[1,1] neg_hi:[1,0]
	v_pk_fma_f32 v[58:59], v[10:11], v[58:59], v[88:89] op_sel_hi:[0,1,1] neg_lo:[1,0,0] neg_hi:[1,0,0]
	v_pk_add_f32 v[88:89], v[60:61], v[90:91]
	v_pk_add_f32 v[60:61], v[60:61], v[90:91] neg_lo:[0,1] neg_hi:[0,1]
	v_pk_mul_f32 v[36:37], v[36:37], v[60:61] op_sel:[0,1] op_sel_hi:[0,0] neg_lo:[1,1] neg_hi:[1,0]
	v_pk_fma_f32 v[36:37], v[32:33], v[60:61], v[36:37] op_sel_hi:[0,1,1] neg_lo:[1,0,0] neg_hi:[1,0,0]
	v_pk_add_f32 v[32:33], v[76:77], v[82:83]
	v_pk_add_f32 v[60:61], v[76:77], v[82:83] neg_lo:[0,1] neg_hi:[0,1]
	v_pk_add_f32 v[76:77], v[54:55], v[40:41]
	v_pk_add_f32 v[40:41], v[40:41], v[54:55] neg_lo:[0,1] neg_hi:[0,1]
	v_pk_mul_f32 v[54:55], v[10:11], v[40:41] op_sel:[0,1] op_sel_hi:[0,0] neg_lo:[1,1] neg_hi:[1,0]
	v_pk_fma_f32 v[54:55], v[10:11], v[40:41], v[54:55] op_sel_hi:[0,1,1]
	v_pk_add_f32 v[40:41], v[78:79], v[86:87]
	v_pk_add_f32 v[78:79], v[78:79], v[86:87] neg_lo:[0,1] neg_hi:[0,1]
	v_xor_b32_e32 v83, 0x80000000, v78
	v_mov_b32_e32 v82, v79
	v_pk_add_f32 v[78:79], v[48:49], v[88:89]
	v_pk_add_f32 v[48:49], v[48:49], v[88:89] neg_lo:[0,1] neg_hi:[0,1]
	v_pk_add_f32 v[88:89], v[76:77], v[78:79]
	v_pk_mul_f32 v[86:87], v[10:11], v[48:49] op_sel:[0,1] op_sel_hi:[0,0] neg_lo:[1,1] neg_hi:[1,0]
	v_pk_fma_f32 v[48:49], v[10:11], v[48:49], v[86:87] op_sel_hi:[0,1,1] neg_lo:[1,0,0] neg_hi:[1,0,0]
	v_pk_add_f32 v[86:87], v[32:33], v[40:41]
	v_pk_add_f32 v[32:33], v[32:33], v[40:41] neg_lo:[0,1] neg_hi:[0,1]
	v_pk_add_f32 v[40:41], v[76:77], v[78:79] neg_lo:[0,1] neg_hi:[0,1]
	v_pk_add_f32 v[78:79], v[86:87], v[88:89] neg_lo:[0,1] neg_hi:[0,1]
	v_pk_add_f32 v[90:91], v[32:33], v[40:41] op_sel:[0,1] op_sel_hi:[1,0] neg_hi:[0,1]
	v_pk_add_f32 v[40:41], v[32:33], v[40:41] op_sel:[0,1] op_sel_hi:[1,0] neg_lo:[0,1]
	v_pk_add_f32 v[76:77], v[54:55], v[48:49]
	v_pk_add_f32 v[48:49], v[54:55], v[48:49] neg_lo:[0,1] neg_hi:[0,1]
	v_pk_add_f32 v[32:33], v[60:61], v[82:83]
	v_pk_add_f32 v[60:61], v[60:61], v[82:83] neg_lo:[0,1] neg_hi:[0,1]
	v_xor_b32_e32 v55, 0x80000000, v48
	v_mov_b32_e32 v54, v49
	v_pk_add_f32 v[82:83], v[32:33], v[76:77]
	v_pk_add_f32 v[48:49], v[32:33], v[76:77] neg_lo:[0,1] neg_hi:[0,1]
	v_pk_add_f32 v[76:77], v[60:61], v[54:55]
	v_pk_add_f32 v[32:33], v[60:61], v[54:55] neg_lo:[0,1] neg_hi:[0,1]
	v_pk_add_f32 v[54:55], v[92:93], v[84:85]
	v_pk_add_f32 v[60:61], v[92:93], v[84:85] neg_lo:[0,1] neg_hi:[0,1]
	v_pk_add_f32 v[84:85], v[56:57], v[44:45]
	v_pk_add_f32 v[44:45], v[44:45], v[56:57] neg_lo:[0,1] neg_hi:[0,1]
	v_pk_add_f32 v[86:87], v[86:87], v[88:89]
	v_pk_mul_f32 v[56:57], v[10:11], v[44:45] op_sel:[0,1] op_sel_hi:[0,0] neg_lo:[1,1] neg_hi:[1,0]
	v_pk_fma_f32 v[56:57], v[10:11], v[44:45], v[56:57] op_sel_hi:[0,1,1]
	v_pk_add_f32 v[44:45], v[80:81], v[58:59]
	v_pk_add_f32 v[58:59], v[80:81], v[58:59] neg_lo:[0,1] neg_hi:[0,1]
	v_xor_b32_e32 v81, 0x80000000, v58
	v_mov_b32_e32 v80, v59
	v_pk_add_f32 v[58:59], v[52:53], v[36:37]
	v_pk_add_f32 v[36:37], v[52:53], v[36:37] neg_lo:[0,1] neg_hi:[0,1]
	v_pk_mul_f32 v[52:53], v[10:11], v[36:37] op_sel:[0,1] op_sel_hi:[0,0] neg_lo:[1,1] neg_hi:[1,0]
	v_pk_fma_f32 v[36:37], v[10:11], v[36:37], v[52:53] op_sel_hi:[0,1,1] neg_lo:[1,0,0] neg_hi:[1,0,0]
	v_pk_add_f32 v[52:53], v[54:55], v[44:45]
	v_pk_add_f32 v[44:45], v[54:55], v[44:45] neg_lo:[0,1] neg_hi:[0,1]
	v_pk_add_f32 v[54:55], v[84:85], v[58:59]
	v_pk_add_f32 v[58:59], v[84:85], v[58:59] neg_lo:[0,1] neg_hi:[0,1]
	v_xor_b32_e32 v85, 0x80000000, v58
	v_mov_b32_e32 v84, v59
	v_pk_add_f32 v[58:59], v[52:53], v[54:55]
	v_pk_add_f32 v[52:53], v[52:53], v[54:55] neg_lo:[0,1] neg_hi:[0,1]
	v_pk_add_f32 v[54:55], v[44:45], v[84:85]
	v_pk_add_f32 v[44:45], v[44:45], v[84:85] neg_lo:[0,1] neg_hi:[0,1]
	v_pk_add_f32 v[84:85], v[60:61], v[80:81]
	v_pk_add_f32 v[60:61], v[60:61], v[80:81] neg_lo:[0,1] neg_hi:[0,1]
	v_pk_add_f32 v[80:81], v[56:57], v[36:37]
	v_pk_add_f32 v[36:37], v[56:57], v[36:37] neg_lo:[0,1] neg_hi:[0,1]
	v_pk_add_f32 v[92:93], v[84:85], v[80:81]
	v_pk_add_f32 v[80:81], v[84:85], v[80:81] neg_lo:[0,1] neg_hi:[0,1]
	v_pk_add_f32 v[84:85], v[60:61], v[36:37] op_sel:[0,1] op_sel_hi:[1,0] neg_hi:[0,1]
	v_pk_add_f32 v[36:37], v[60:61], v[36:37] op_sel:[0,1] op_sel_hi:[1,0] neg_lo:[0,1]
	v_pk_fma_f32 v[60:61], v[16:17], s[90:91], v[16:17] op_sel:[1,0,0] op_sel_hi:[0,1,1]
	v_pk_mul_f32 v[56:57], v[94:95], s[14:15] op_sel:[1,0] neg_lo:[1,0]
	v_pk_mul_f32 v[88:89], v[60:61], v[86:87] op_sel:[1,1] op_sel_hi:[0,1] neg_lo:[0,1]
	v_pk_fma_f32 v[56:57], v[94:95], s[94:95], v[56:57] op_sel_hi:[0,1,1]
	v_pk_fma_f32 v[86:87], v[60:61], v[86:87], v[88:89] op_sel_hi:[1,0,1]
	ds_write2_b64 v75, v[56:57], v[86:87] offset1:16
	v_pk_mul_f32 v[56:57], v[16:17], v[60:61] op_sel:[1,1] op_sel_hi:[0,1] neg_lo:[0,1]
	v_pk_fma_f32 v[56:57], v[16:17], v[60:61], v[56:57] op_sel_hi:[1,0,1]
	v_pk_mul_f32 v[60:61], v[56:57], v[102:103] op_sel:[1,1] op_sel_hi:[0,1] neg_lo:[0,1]
	v_pk_mul_f32 v[86:87], v[16:17], v[56:57] op_sel:[1,1] op_sel_hi:[0,1] neg_lo:[0,1]
	v_pk_fma_f32 v[60:61], v[56:57], v[102:103], v[60:61] op_sel_hi:[1,0,1]
	v_pk_fma_f32 v[56:57], v[16:17], v[56:57], v[86:87] op_sel_hi:[1,0,1]
	v_pk_mul_f32 v[86:87], v[56:57], v[58:59] op_sel:[1,1] op_sel_hi:[0,1] neg_lo:[0,1]
	v_pk_fma_f32 v[58:59], v[56:57], v[58:59], v[86:87] op_sel_hi:[1,0,1]
	ds_write2_b64 v74, v[60:61], v[58:59] offset0:32 offset1:48
	v_pk_mul_f32 v[58:59], v[16:17], v[56:57] op_sel:[1,1] op_sel_hi:[0,1] neg_lo:[0,1]
	v_pk_fma_f32 v[56:57], v[16:17], v[56:57], v[58:59] op_sel_hi:[1,0,1]
	v_pk_mul_f32 v[58:59], v[56:57], v[104:105] op_sel:[1,1] op_sel_hi:[0,1] neg_lo:[0,1]
	v_pk_mul_f32 v[60:61], v[16:17], v[56:57] op_sel:[1,1] op_sel_hi:[0,1] neg_lo:[0,1]
	v_pk_fma_f32 v[58:59], v[56:57], v[104:105], v[58:59] op_sel_hi:[1,0,1]
	v_pk_fma_f32 v[56:57], v[16:17], v[56:57], v[60:61] op_sel_hi:[1,0,1]
	v_pk_mul_f32 v[60:61], v[56:57], v[82:83] op_sel:[1,1] op_sel_hi:[0,1] neg_lo:[0,1]
	v_pk_fma_f32 v[60:61], v[56:57], v[82:83], v[60:61] op_sel_hi:[1,0,1]
	ds_write2_b64 v73, v[58:59], v[60:61] offset0:64 offset1:80
	v_pk_mul_f32 v[58:59], v[16:17], v[56:57] op_sel:[1,1] op_sel_hi:[0,1] neg_lo:[0,1]
	v_pk_fma_f32 v[56:57], v[16:17], v[56:57], v[58:59] op_sel_hi:[1,0,1]
	v_pk_mul_f32 v[58:59], v[56:57], v[98:99] op_sel:[1,1] op_sel_hi:[0,1] neg_lo:[0,1]
	v_pk_mul_f32 v[60:61], v[16:17], v[56:57] op_sel:[1,1] op_sel_hi:[0,1] neg_lo:[0,1]
	v_pk_fma_f32 v[58:59], v[56:57], v[98:99], v[58:59] op_sel_hi:[1,0,1]
	v_pk_fma_f32 v[56:57], v[16:17], v[56:57], v[60:61] op_sel_hi:[1,0,1]
	v_pk_mul_f32 v[60:61], v[56:57], v[92:93] op_sel:[1,1] op_sel_hi:[0,1] neg_lo:[0,1]
	v_pk_fma_f32 v[60:61], v[56:57], v[92:93], v[60:61] op_sel_hi:[1,0,1]
	ds_write2_b64 v72, v[58:59], v[60:61] offset0:96 offset1:112
	v_pk_mul_f32 v[58:59], v[16:17], v[56:57] op_sel:[1,1] op_sel_hi:[0,1] neg_lo:[0,1]
	v_pk_fma_f32 v[56:57], v[16:17], v[56:57], v[58:59] op_sel_hi:[1,0,1]
	v_pk_mul_f32 v[58:59], v[56:57], v[46:47] op_sel:[1,1] op_sel_hi:[0,1] neg_lo:[0,1]
	v_pk_fma_f32 v[46:47], v[56:57], v[46:47], v[58:59] op_sel_hi:[1,0,1]
	v_pk_mul_f32 v[58:59], v[16:17], v[56:57] op_sel:[1,1] op_sel_hi:[0,1] neg_lo:[0,1]
	v_pk_fma_f32 v[56:57], v[16:17], v[56:57], v[58:59] op_sel_hi:[1,0,1]
	v_pk_mul_f32 v[58:59], v[56:57], v[90:91] op_sel:[1,1] op_sel_hi:[0,1] neg_lo:[0,1]
	v_pk_fma_f32 v[58:59], v[56:57], v[90:91], v[58:59] op_sel_hi:[1,0,1]
	ds_write2_b64 v71, v[46:47], v[58:59] offset0:128 offset1:144
	v_pk_mul_f32 v[46:47], v[16:17], v[56:57] op_sel:[1,1] op_sel_hi:[0,1] neg_lo:[0,1]
	v_pk_fma_f32 v[46:47], v[16:17], v[56:57], v[46:47] op_sel_hi:[1,0,1]
	v_pk_mul_f32 v[56:57], v[46:47], v[50:51] op_sel:[1,1] op_sel_hi:[0,1] neg_lo:[0,1]
	v_pk_fma_f32 v[50:51], v[46:47], v[50:51], v[56:57] op_sel_hi:[1,0,1]
	v_pk_mul_f32 v[56:57], v[16:17], v[46:47] op_sel:[1,1] op_sel_hi:[0,1] neg_lo:[0,1]
	v_pk_fma_f32 v[46:47], v[16:17], v[46:47], v[56:57] op_sel_hi:[1,0,1]
	v_pk_mul_f32 v[56:57], v[46:47], v[54:55] op_sel:[1,1] op_sel_hi:[0,1] neg_lo:[0,1]
	v_pk_fma_f32 v[54:55], v[46:47], v[54:55], v[56:57] op_sel_hi:[1,0,1]
	ds_write2_b64 v70, v[50:51], v[54:55] offset0:160 offset1:176
	v_pk_mul_f32 v[50:51], v[16:17], v[46:47] op_sel:[1,1] op_sel_hi:[0,1] neg_lo:[0,1]
	v_pk_fma_f32 v[46:47], v[16:17], v[46:47], v[50:51] op_sel_hi:[1,0,1]
	v_pk_mul_f32 v[50:51], v[38:39], v[46:47] op_sel:[1,1] op_sel_hi:[1,0] neg_lo:[1,0]
	v_pk_fma_f32 v[38:39], v[38:39], v[46:47], v[50:51] op_sel_hi:[0,1,1]
	v_pk_mul_f32 v[50:51], v[16:17], v[46:47] op_sel:[1,1] op_sel_hi:[0,1] neg_lo:[0,1]
	v_pk_fma_f32 v[46:47], v[16:17], v[46:47], v[50:51] op_sel_hi:[1,0,1]
	v_pk_mul_f32 v[50:51], v[46:47], v[76:77] op_sel:[1,1] op_sel_hi:[0,1] neg_lo:[0,1]
	v_pk_fma_f32 v[50:51], v[46:47], v[76:77], v[50:51] op_sel_hi:[1,0,1]
	ds_write2_b64 v69, v[38:39], v[50:51] offset0:192 offset1:208
	v_pk_mul_f32 v[38:39], v[16:17], v[46:47] op_sel:[1,1] op_sel_hi:[0,1] neg_lo:[0,1]
	v_pk_fma_f32 v[38:39], v[16:17], v[46:47], v[38:39] op_sel_hi:[1,0,1]
	v_pk_mul_f32 v[46:47], v[42:43], v[38:39] op_sel:[1,1] op_sel_hi:[1,0] neg_lo:[1,0]
	v_pk_fma_f32 v[42:43], v[42:43], v[38:39], v[46:47] op_sel_hi:[0,1,1]
	v_pk_mul_f32 v[46:47], v[16:17], v[38:39] op_sel:[1,1] op_sel_hi:[0,1] neg_lo:[0,1]
	v_pk_fma_f32 v[38:39], v[16:17], v[38:39], v[46:47] op_sel_hi:[1,0,1]
	v_pk_mul_f32 v[46:47], v[38:39], v[84:85] op_sel:[1,1] op_sel_hi:[0,1] neg_lo:[0,1]
	v_pk_fma_f32 v[46:47], v[38:39], v[84:85], v[46:47] op_sel_hi:[1,0,1]
	ds_write2_b64 v68, v[42:43], v[46:47] offset0:224 offset1:240
	v_pk_mul_f32 v[42:43], v[16:17], v[38:39] op_sel:[1,1] op_sel_hi:[0,1] neg_lo:[0,1]
	v_pk_fma_f32 v[38:39], v[16:17], v[38:39], v[42:43] op_sel_hi:[1,0,1]
	v_pk_mul_f32 v[42:43], v[30:31], v[38:39] op_sel:[1,1] op_sel_hi:[1,0] neg_lo:[1,0]
	v_pk_fma_f32 v[30:31], v[30:31], v[38:39], v[42:43] op_sel_hi:[0,1,1]
	v_pk_mul_f32 v[42:43], v[16:17], v[38:39] op_sel:[1,1] op_sel_hi:[0,1] neg_lo:[0,1]
	v_pk_fma_f32 v[38:39], v[16:17], v[38:39], v[42:43] op_sel_hi:[1,0,1]
	v_pk_mul_f32 v[42:43], v[78:79], v[38:39] op_sel:[1,1] op_sel_hi:[1,0] neg_lo:[1,0]
	v_pk_fma_f32 v[42:43], v[78:79], v[38:39], v[42:43] op_sel_hi:[0,1,1]
	ds_write2_b64 v67, v[30:31], v[42:43] offset1:16
	v_pk_mul_f32 v[30:31], v[16:17], v[38:39] op_sel:[1,1] op_sel_hi:[0,1] neg_lo:[0,1]
	v_pk_fma_f32 v[30:31], v[16:17], v[38:39], v[30:31] op_sel_hi:[1,0,1]
	v_pk_mul_f32 v[38:39], v[34:35], v[30:31] op_sel:[1,1] op_sel_hi:[1,0] neg_lo:[1,0]
	v_pk_fma_f32 v[34:35], v[34:35], v[30:31], v[38:39] op_sel_hi:[0,1,1]
	v_pk_mul_f32 v[38:39], v[16:17], v[30:31] op_sel:[1,1] op_sel_hi:[0,1] neg_lo:[0,1]
	v_pk_fma_f32 v[30:31], v[16:17], v[30:31], v[38:39] op_sel_hi:[1,0,1]
	v_pk_mul_f32 v[38:39], v[52:53], v[30:31] op_sel:[1,1] op_sel_hi:[1,0] neg_lo:[1,0]
	v_pk_fma_f32 v[38:39], v[52:53], v[30:31], v[38:39] op_sel_hi:[0,1,1]
	ds_write2_b64 v66, v[34:35], v[38:39] offset0:32 offset1:48
	v_pk_mul_f32 v[34:35], v[16:17], v[30:31] op_sel:[1,1] op_sel_hi:[0,1] neg_lo:[0,1]
	v_pk_fma_f32 v[30:31], v[16:17], v[30:31], v[34:35] op_sel_hi:[1,0,1]
	v_pk_mul_f32 v[34:35], v[26:27], v[30:31] op_sel:[1,1] op_sel_hi:[1,0] neg_lo:[1,0]
	v_pk_fma_f32 v[26:27], v[26:27], v[30:31], v[34:35] op_sel_hi:[0,1,1]
	v_pk_mul_f32 v[34:35], v[16:17], v[30:31] op_sel:[1,1] op_sel_hi:[0,1] neg_lo:[0,1]
	v_pk_fma_f32 v[30:31], v[16:17], v[30:31], v[34:35] op_sel_hi:[1,0,1]
	v_pk_mul_f32 v[34:35], v[48:49], v[30:31] op_sel:[1,1] op_sel_hi:[1,0] neg_lo:[1,0]
	v_pk_fma_f32 v[34:35], v[48:49], v[30:31], v[34:35] op_sel_hi:[0,1,1]
	ds_write2_b64 v65, v[26:27], v[34:35] offset0:64 offset1:80
	v_pk_mul_f32 v[26:27], v[16:17], v[30:31] op_sel:[1,1] op_sel_hi:[0,1] neg_lo:[0,1]
	v_pk_fma_f32 v[26:27], v[16:17], v[30:31], v[26:27] op_sel_hi:[1,0,1]
	v_pk_mul_f32 v[30:31], v[28:29], v[26:27] op_sel:[1,1] op_sel_hi:[1,0] neg_lo:[1,0]
	v_pk_fma_f32 v[28:29], v[28:29], v[26:27], v[30:31] op_sel_hi:[0,1,1]
	v_pk_mul_f32 v[30:31], v[16:17], v[26:27] op_sel:[1,1] op_sel_hi:[0,1] neg_lo:[0,1]
	v_pk_fma_f32 v[26:27], v[16:17], v[26:27], v[30:31] op_sel_hi:[1,0,1]
	v_pk_mul_f32 v[30:31], v[80:81], v[26:27] op_sel:[1,1] op_sel_hi:[1,0] neg_lo:[1,0]
	v_pk_fma_f32 v[30:31], v[80:81], v[26:27], v[30:31] op_sel_hi:[0,1,1]
	ds_write2_b64 v64, v[28:29], v[30:31] offset0:96 offset1:112
	v_pk_mul_f32 v[28:29], v[16:17], v[26:27] op_sel:[1,1] op_sel_hi:[0,1] neg_lo:[0,1]
	v_pk_fma_f32 v[26:27], v[16:17], v[26:27], v[28:29] op_sel_hi:[1,0,1]
	v_pk_mul_f32 v[28:29], v[22:23], v[26:27] op_sel:[1,1] op_sel_hi:[1,0] neg_lo:[1,0]
	v_pk_fma_f32 v[22:23], v[22:23], v[26:27], v[28:29] op_sel_hi:[0,1,1]
	v_pk_mul_f32 v[28:29], v[16:17], v[26:27] op_sel:[1,1] op_sel_hi:[0,1] neg_lo:[0,1]
	v_pk_fma_f32 v[26:27], v[16:17], v[26:27], v[28:29] op_sel_hi:[1,0,1]
	v_pk_mul_f32 v[28:29], v[40:41], v[26:27] op_sel:[1,1] op_sel_hi:[1,0] neg_lo:[1,0]
	v_pk_fma_f32 v[28:29], v[40:41], v[26:27], v[28:29] op_sel_hi:[0,1,1]
	ds_write2_b64 v63, v[22:23], v[28:29] offset0:128 offset1:144
	v_pk_mul_f32 v[22:23], v[16:17], v[26:27] op_sel:[1,1] op_sel_hi:[0,1] neg_lo:[0,1]
	v_pk_fma_f32 v[22:23], v[16:17], v[26:27], v[22:23] op_sel_hi:[1,0,1]
	v_pk_mul_f32 v[26:27], v[24:25], v[22:23] op_sel:[1,1] op_sel_hi:[1,0] neg_lo:[1,0]
	v_pk_fma_f32 v[24:25], v[24:25], v[22:23], v[26:27] op_sel_hi:[0,1,1]
	v_pk_mul_f32 v[26:27], v[16:17], v[22:23] op_sel:[1,1] op_sel_hi:[0,1] neg_lo:[0,1]
	v_pk_fma_f32 v[22:23], v[16:17], v[22:23], v[26:27] op_sel_hi:[1,0,1]
	v_pk_mul_f32 v[26:27], v[44:45], v[22:23] op_sel:[1,1] op_sel_hi:[1,0] neg_lo:[1,0]
	v_pk_fma_f32 v[26:27], v[44:45], v[22:23], v[26:27] op_sel_hi:[0,1,1]
	ds_write2_b64 v62, v[24:25], v[26:27] offset0:160 offset1:176
	v_pk_mul_f32 v[24:25], v[16:17], v[22:23] op_sel:[1,1] op_sel_hi:[0,1] neg_lo:[0,1]
	v_pk_fma_f32 v[22:23], v[16:17], v[22:23], v[24:25] op_sel_hi:[1,0,1]
	v_pk_mul_f32 v[24:25], v[18:19], v[22:23] op_sel:[1,1] op_sel_hi:[1,0] neg_lo:[1,0]
	v_pk_fma_f32 v[18:19], v[18:19], v[22:23], v[24:25] op_sel_hi:[0,1,1]
	v_pk_mul_f32 v[24:25], v[16:17], v[22:23] op_sel:[1,1] op_sel_hi:[0,1] neg_lo:[0,1]
	v_pk_fma_f32 v[22:23], v[16:17], v[22:23], v[24:25] op_sel_hi:[1,0,1]
	v_pk_mul_f32 v[24:25], v[32:33], v[22:23] op_sel:[1,1] op_sel_hi:[1,0] neg_lo:[1,0]
	v_pk_fma_f32 v[24:25], v[32:33], v[22:23], v[24:25] op_sel_hi:[0,1,1]
	ds_write2_b64 v15, v[18:19], v[24:25] offset0:192 offset1:208
	v_pk_mul_f32 v[18:19], v[16:17], v[22:23] op_sel:[1,1] op_sel_hi:[0,1] neg_lo:[0,1]
	v_pk_fma_f32 v[18:19], v[16:17], v[22:23], v[18:19] op_sel_hi:[1,0,1]
	v_pk_mul_f32 v[22:23], v[20:21], v[18:19] op_sel:[1,1] op_sel_hi:[1,0] neg_lo:[1,0]
	v_pk_fma_f32 v[20:21], v[20:21], v[18:19], v[22:23] op_sel_hi:[0,1,1]
	v_pk_mul_f32 v[22:23], v[16:17], v[18:19] op_sel:[1,1] op_sel_hi:[0,1] neg_lo:[0,1]
	v_pk_fma_f32 v[16:17], v[16:17], v[18:19], v[22:23] op_sel_hi:[1,0,1]
	v_pk_mul_f32 v[18:19], v[36:37], v[16:17] op_sel:[1,1] op_sel_hi:[1,0] neg_lo:[1,0]
	v_pk_fma_f32 v[16:17], v[36:37], v[16:17], v[18:19] op_sel_hi:[0,1,1]
	ds_write2_b64 v13, v[20:21], v[16:17] offset0:224 offset1:240
	v_mov_b32_e32 v16, v182
	v_mov_b32_e32 v10, v176
	v_mov_b32_e32 v17, v175
	s_waitcnt lgkmcnt(0)
	s_barrier
	v_lshlrev_b32_e32 v190, 3, v16
	v_add_u32_e32 v190, 0x1000, v190
	global_load_dwordx2 v[202:203], v190, s[46:47] offset:-4096
	global_load_dwordx2 v[204:205], v190, s[46:47]
	v_add_u32_e32 v190, 0x2000, v190
	global_load_dwordx2 v[206:207], v190, s[46:47] offset:-4096
	global_load_dwordx2 v[208:209], v190, s[46:47]
	v_add_u32_e32 v190, 0x2000, v190
	global_load_dwordx2 v[210:211], v190, s[46:47] offset:-4096
	global_load_dwordx2 v[212:213], v190, s[46:47]
	v_add_u32_e32 v190, 0x2000, v190
	global_load_dwordx2 v[214:215], v190, s[46:47] offset:-4096
	global_load_dwordx2 v[216:217], v190, s[46:47]
	v_add_u32_e32 v190, 0x2000, v190
	global_load_dwordx2 v[218:219], v190, s[46:47] offset:-4096
	global_load_dwordx2 v[220:221], v190, s[46:47]
	v_add_u32_e32 v190, 0x2000, v190
	global_load_dwordx2 v[222:223], v190, s[46:47] offset:-4096
	global_load_dwordx2 v[224:225], v190, s[46:47]
	v_add_u32_e32 v190, 0x2000, v190
	global_load_dwordx2 v[226:227], v190, s[46:47] offset:-4096
	global_load_dwordx2 v[228:229], v190, s[46:47]
	v_add_u32_e32 v190, 0x2000, v190
	global_load_dwordx2 v[230:231], v190, s[46:47] offset:-4096
	global_load_dwordx2 v[232:233], v190, s[46:47]
	v_mov_b32_e32 v50, v165
	v_lshlrev_b32_e32 v13, 3, v17
	v_lshlrev_b32_e32 v48, 3, v10
	v_add3_u32 v10, 0, v13, v48
	v_xor_b32_e32 v13, 1, v17
	v_xor_b32_e32 v34, 8, v17
	v_xor_b32_e32 v36, 9, v17
	v_lshlrev_b32_e32 v13, 3, v13
	v_xor_b32_e32 v15, 2, v17
	v_xor_b32_e32 v24, 3, v17
	v_xor_b32_e32 v26, 4, v17
	v_xor_b32_e32 v28, 5, v17
	v_xor_b32_e32 v30, 6, v17
	v_xor_b32_e32 v32, 7, v17
	v_lshlrev_b32_e32 v34, 3, v34
	v_lshlrev_b32_e32 v36, 3, v36
	v_xor_b32_e32 v38, 10, v17
	v_xor_b32_e32 v40, 11, v17
	v_xor_b32_e32 v42, 12, v17
	v_xor_b32_e32 v44, 13, v17
	v_xor_b32_e32 v46, 14, v17
	v_xor_b32_e32 v17, 15, v17
	v_add3_u32 v13, 0, v13, v48
	v_lshlrev_b32_e32 v15, 3, v15
	v_lshlrev_b32_e32 v24, 3, v24
	v_lshlrev_b32_e32 v26, 3, v26
	v_lshlrev_b32_e32 v28, 3, v28
	v_lshlrev_b32_e32 v30, 3, v30
	v_lshlrev_b32_e32 v32, 3, v32
	v_add3_u32 v57, 0, v34, v48
	v_add3_u32 v58, 0, v36, v48
	v_lshlrev_b32_e32 v38, 3, v38
	v_lshlrev_b32_e32 v40, 3, v40
	v_lshlrev_b32_e32 v42, 3, v42
	v_lshlrev_b32_e32 v44, 3, v44
	v_lshlrev_b32_e32 v46, 3, v46
	v_lshlrev_b32_e32 v17, 3, v17
	ds_read_b64 v[18:19], v10
	ds_read_b64 v[20:21], v13
	v_add3_u32 v15, 0, v15, v48
	v_add3_u32 v52, 0, v24, v48
	v_add3_u32 v53, 0, v26, v48
	v_add3_u32 v54, 0, v28, v48
	v_add3_u32 v55, 0, v30, v48
	v_add3_u32 v56, 0, v32, v48
	ds_read_b64 v[34:35], v57
	ds_read_b64 v[36:37], v58
	v_add3_u32 v59, 0, v38, v48
	v_add3_u32 v60, 0, v40, v48
	v_add3_u32 v61, 0, v42, v48
	v_add3_u32 v62, 0, v44, v48
	v_add3_u32 v63, 0, v46, v48
	v_add3_u32 v64, 0, v17, v48
	v_mov_b32_e32 v17, v1
	ds_read_b64 v[22:23], v15
	ds_read_b64 v[24:25], v52
	ds_read_b64 v[26:27], v53
	ds_read_b64 v[28:29], v54
	ds_read_b64 v[30:31], v55
	ds_read_b64 v[32:33], v56
	ds_read_b64 v[38:39], v59
	ds_read_b64 v[40:41], v60
	ds_read_b64 v[42:43], v61
	ds_read_b64 v[44:45], v62
	ds_read_b64 v[46:47], v63
	ds_read_b64 v[48:49], v64
	s_waitcnt lgkmcnt(13)
	v_pk_add_f32 v[70:71], v[18:19], v[34:35]
	v_mov_b32_e32 v17, v164
	v_pk_add_f32 v[18:19], v[18:19], v[34:35] neg_lo:[0,1] neg_hi:[0,1]
	v_mov_b32_e32 v17, v166
	s_waitcnt lgkmcnt(12)
	v_pk_add_f32 v[34:35], v[20:21], v[36:37]
	v_pk_add_f32 v[20:21], v[20:21], v[36:37] neg_lo:[0,1] neg_hi:[0,1]
	v_mov_b32_e32 v66, v167
	v_mov_b32_e32 v17, v168
	v_mov_b32_e32 v68, v169
	s_nop 0
	v_pk_mul_f32 v[36:37], v[20:21], v[68:69] op_sel:[1,0] op_sel_hi:[0,0] neg_lo:[1,1] neg_hi:[0,1]
	v_mov_b32_e32 v17, v170
	v_pk_fma_f32 v[20:21], v[20:21], v[50:51], v[36:37] op_sel_hi:[1,0,1]
	s_waitcnt lgkmcnt(5)
	v_pk_add_f32 v[36:37], v[22:23], v[38:39]
	v_pk_add_f32 v[22:23], v[22:23], v[38:39] neg_lo:[0,1] neg_hi:[0,1]
	v_pk_mul_f32 v[38:39], v[22:23], v[66:67] op_sel:[1,0] op_sel_hi:[0,0] neg_lo:[1,1] neg_hi:[0,1]
	v_mov_b32_e32 v17, v171
	v_pk_fma_f32 v[22:23], v[22:23], v[66:67], v[38:39] op_sel_hi:[1,0,1]
	s_waitcnt lgkmcnt(4)
	v_pk_add_f32 v[38:39], v[24:25], v[40:41]
	v_pk_add_f32 v[24:25], v[24:25], v[40:41] neg_lo:[0,1] neg_hi:[0,1]
	v_pk_mul_f32 v[40:41], v[24:25], v[68:69] op_sel_hi:[1,0]
	v_pk_fma_f32 v[24:25], v[24:25], v[50:51], v[40:41] op_sel:[1,0,0] op_sel_hi:[0,0,1] neg_lo:[1,1,0] neg_hi:[0,1,0]
	s_waitcnt lgkmcnt(3)
	v_pk_add_f32 v[40:41], v[26:27], v[42:43]
	v_pk_add_f32 v[26:27], v[26:27], v[42:43] neg_lo:[0,1] neg_hi:[0,1]
	v_ashrrev_i32_e32 v17, 31, v16
	v_xor_b32_e32 v73, 0x80000000, v26
	v_mov_b32_e32 v72, v27
	s_waitcnt lgkmcnt(2)
	v_pk_add_f32 v[26:27], v[28:29], v[44:45]
	v_pk_add_f32 v[28:29], v[28:29], v[44:45] neg_lo:[0,1] neg_hi:[0,1]
	v_pk_mul_f32 v[42:43], v[28:29], v[68:69] op_sel_hi:[1,0] neg_lo:[0,1] neg_hi:[0,1]
	v_pk_fma_f32 v[28:29], v[28:29], v[50:51], v[42:43] op_sel:[1,0,0] op_sel_hi:[0,0,1] neg_lo:[1,1,0] neg_hi:[0,1,0]
	s_waitcnt lgkmcnt(1)
	v_pk_add_f32 v[42:43], v[30:31], v[46:47]
	v_pk_add_f32 v[30:31], v[30:31], v[46:47] neg_lo:[0,1] neg_hi:[0,1]
	v_pk_mul_f32 v[44:45], v[30:31], v[66:67] op_sel:[1,0] op_sel_hi:[0,0] neg_lo:[1,1] neg_hi:[0,1]
	v_pk_fma_f32 v[30:31], v[30:31], v[66:67], v[44:45] op_sel_hi:[1,0,1] neg_lo:[0,1,0] neg_hi:[0,1,0]
	s_waitcnt lgkmcnt(0)
	v_pk_add_f32 v[44:45], v[32:33], v[48:49]
	v_pk_add_f32 v[32:33], v[32:33], v[48:49] neg_lo:[0,1] neg_hi:[0,1]
	v_pk_add_f32 v[48:49], v[34:35], v[26:27]
	v_pk_add_f32 v[26:27], v[34:35], v[26:27] neg_lo:[0,1] neg_hi:[0,1]
	v_pk_mul_f32 v[34:35], v[26:27], v[66:67] op_sel:[1,0] op_sel_hi:[0,0] neg_lo:[1,1] neg_hi:[0,1]
	v_pk_fma_f32 v[26:27], v[26:27], v[66:67], v[34:35] op_sel_hi:[1,0,1]
	v_pk_add_f32 v[34:35], v[36:37], v[42:43]
	v_pk_add_f32 v[36:37], v[36:37], v[42:43] neg_lo:[0,1] neg_hi:[0,1]
	v_pk_mul_f32 v[46:47], v[32:33], v[68:69] op_sel:[1,0] op_sel_hi:[0,0] neg_lo:[1,1] neg_hi:[0,1]
	v_xor_b32_e32 v43, 0x80000000, v36
	v_mov_b32_e32 v42, v37
	v_pk_add_f32 v[36:37], v[38:39], v[44:45]
	v_pk_add_f32 v[38:39], v[38:39], v[44:45] neg_lo:[0,1] neg_hi:[0,1]
	v_pk_fma_f32 v[46:47], v[32:33], v[50:51], v[46:47] op_sel_hi:[1,0,1] neg_lo:[0,1,0] neg_hi:[0,1,0]
	v_pk_add_f32 v[32:33], v[70:71], v[40:41]
	v_pk_mul_f32 v[44:45], v[38:39], v[66:67] op_sel:[1,0] op_sel_hi:[0,0] neg_lo:[1,1] neg_hi:[0,1]
	v_pk_add_f32 v[40:41], v[70:71], v[40:41] neg_lo:[0,1] neg_hi:[0,1]
	v_pk_fma_f32 v[38:39], v[38:39], v[66:67], v[44:45] op_sel_hi:[1,0,1] neg_lo:[0,1,0] neg_hi:[0,1,0]
	v_pk_add_f32 v[44:45], v[32:33], v[34:35]
	v_pk_add_f32 v[32:33], v[32:33], v[34:35] neg_lo:[0,1] neg_hi:[0,1]
	v_pk_add_f32 v[34:35], v[48:49], v[36:37]
	v_pk_add_f32 v[36:37], v[48:49], v[36:37] neg_lo:[0,1] neg_hi:[0,1]
	v_pk_add_f32 v[50:51], v[44:45], v[34:35]
	v_xor_b32_e32 v49, 0x80000000, v36
	v_mov_b32_e32 v48, v37
	v_pk_add_f32 v[36:37], v[44:45], v[34:35] neg_lo:[0,1] neg_hi:[0,1]
	v_pk_add_f32 v[68:69], v[32:33], v[48:49]
	v_pk_add_f32 v[44:45], v[32:33], v[48:49] neg_lo:[0,1] neg_hi:[0,1]
	v_pk_add_f32 v[32:33], v[40:41], v[42:43]
	v_pk_add_f32 v[34:35], v[40:41], v[42:43] neg_lo:[0,1] neg_hi:[0,1]
	v_pk_add_f32 v[40:41], v[26:27], v[38:39]
	v_pk_add_f32 v[26:27], v[26:27], v[38:39] neg_lo:[0,1] neg_hi:[0,1]
	v_pk_add_f32 v[42:43], v[32:33], v[40:41] neg_lo:[0,1] neg_hi:[0,1]
	v_xor_b32_e32 v39, 0x80000000, v26
	v_mov_b32_e32 v38, v27
	v_pk_add_f32 v[26:27], v[32:33], v[40:41]
	v_pk_add_f32 v[40:41], v[20:21], v[28:29]
	v_pk_add_f32 v[20:21], v[20:21], v[28:29] neg_lo:[0,1] neg_hi:[0,1]
	v_pk_add_f32 v[32:33], v[34:35], v[38:39]
	v_pk_mul_f32 v[28:29], v[66:67], v[20:21] op_sel:[0,1] op_sel_hi:[0,0] neg_lo:[1,1] neg_hi:[1,0]
	v_pk_fma_f32 v[20:21], v[66:67], v[20:21], v[28:29] op_sel_hi:[0,1,1]
	v_pk_add_f32 v[28:29], v[22:23], v[30:31]
	v_pk_add_f32 v[22:23], v[22:23], v[30:31] neg_lo:[0,1] neg_hi:[0,1]
	v_pk_add_f32 v[38:39], v[34:35], v[38:39] neg_lo:[0,1] neg_hi:[0,1]
	v_xor_b32_e32 v31, 0x80000000, v22
	v_mov_b32_e32 v30, v23
	v_pk_add_f32 v[22:23], v[24:25], v[46:47]
	v_pk_add_f32 v[24:25], v[24:25], v[46:47] neg_lo:[0,1] neg_hi:[0,1]
	v_pk_add_f32 v[34:35], v[18:19], v[72:73]
	v_pk_mul_f32 v[46:47], v[66:67], v[24:25] op_sel:[0,1] op_sel_hi:[0,0] neg_lo:[1,1] neg_hi:[1,0]
	v_pk_fma_f32 v[24:25], v[66:67], v[24:25], v[46:47] op_sel_hi:[0,1,1] neg_lo:[1,0,0] neg_hi:[1,0,0]
	v_pk_add_f32 v[46:47], v[34:35], v[28:29]
	v_pk_add_f32 v[28:29], v[34:35], v[28:29] neg_lo:[0,1] neg_hi:[0,1]
	v_pk_add_f32 v[34:35], v[40:41], v[22:23]
	v_pk_add_f32 v[22:23], v[40:41], v[22:23] neg_lo:[0,1] neg_hi:[0,1]
	v_pk_add_f32 v[18:19], v[18:19], v[72:73] neg_lo:[0,1] neg_hi:[0,1]
	v_pk_add_f32 v[66:67], v[28:29], v[22:23] op_sel:[0,1] op_sel_hi:[1,0] neg_hi:[0,1]
	v_pk_add_f32 v[48:49], v[28:29], v[22:23] op_sel:[0,1] op_sel_hi:[1,0] neg_lo:[0,1]
	v_pk_add_f32 v[28:29], v[18:19], v[30:31]
	v_pk_add_f32 v[18:19], v[18:19], v[30:31] neg_lo:[0,1] neg_hi:[0,1]
	v_pk_add_f32 v[30:31], v[20:21], v[24:25]
	v_pk_add_f32 v[20:21], v[20:21], v[24:25] neg_lo:[0,1] neg_hi:[0,1]
	v_pk_add_f32 v[22:23], v[46:47], v[34:35]
	v_xor_b32_e32 v25, 0x80000000, v20
	v_mov_b32_e32 v24, v21
	v_lshl_add_u64 v[20:21], v[16:17], 3, s[46:47]
	s_waitcnt vmcnt(0)
	v_pk_add_f32 v[40:41], v[46:47], v[34:35] neg_lo:[0,1] neg_hi:[0,1]
	v_pk_add_f32 v[34:35], v[18:19], v[24:25]
	v_pk_add_f32 v[18:19], v[18:19], v[24:25] neg_lo:[0,1] neg_hi:[0,1]
	v_pk_add_f32 v[70:71], v[28:29], v[30:31]
	v_pk_add_f32 v[46:47], v[28:29], v[30:31] neg_lo:[0,1] neg_hi:[0,1]
	v_mov_b32_e32 v17, v1
	s_nop 0
	v_pk_mul_f32 v[24:25], v[50:51], v[202:203] op_sel:[1,1] op_sel_hi:[1,0] neg_lo:[1,0]
	v_pk_fma_f32 v[20:21], v[50:51], v[202:203], v[24:25] op_sel_hi:[0,1,1]
	v_add_u32_e32 v24, 0x200, v16
	v_ashrrev_i32_e32 v25, 31, v24
	v_lshl_add_u64 v[24:25], v[24:25], 3, s[46:47]
	s_nop 0
	v_pk_mul_f32 v[28:29], v[204:205], v[22:23] op_sel:[1,1] op_sel_hi:[0,1] neg_lo:[0,1]
	v_pk_fma_f32 v[22:23], v[204:205], v[22:23], v[28:29] op_sel_hi:[1,0,1]
	v_add_u32_e32 v24, 0x400, v16
	v_ashrrev_i32_e32 v25, 31, v24
	v_lshl_add_u64 v[24:25], v[24:25], 3, s[46:47]
	s_nop 0
	v_pk_mul_f32 v[28:29], v[26:27], v[206:207] op_sel:[1,1] op_sel_hi:[1,0] neg_lo:[1,0]
	v_pk_fma_f32 v[24:25], v[26:27], v[206:207], v[28:29] op_sel_hi:[0,1,1]
	v_add_u32_e32 v26, 0x600, v16
	v_ashrrev_i32_e32 v27, 31, v26
	v_lshl_add_u64 v[26:27], v[26:27], 3, s[46:47]
	s_nop 0
	v_pk_mul_f32 v[28:29], v[208:209], v[70:71] op_sel:[1,1] op_sel_hi:[0,1] neg_lo:[0,1]
	v_pk_fma_f32 v[26:27], v[208:209], v[70:71], v[28:29] op_sel_hi:[1,0,1]
	v_add_u32_e32 v28, 0x800, v16
	v_ashrrev_i32_e32 v29, 31, v28
	v_lshl_add_u64 v[28:29], v[28:29], 3, s[46:47]
	s_nop 0
	v_pk_mul_f32 v[30:31], v[68:69], v[210:211] op_sel:[1,1] op_sel_hi:[1,0] neg_lo:[1,0]
	v_pk_fma_f32 v[28:29], v[68:69], v[210:211], v[30:31] op_sel_hi:[0,1,1]
	v_add_u32_e32 v30, 0xa00, v16
	v_ashrrev_i32_e32 v31, 31, v30
	v_lshl_add_u64 v[30:31], v[30:31], 3, s[46:47]
	v_mov_b32_e32 v68, v169
	s_nop 0
	v_pk_mul_f32 v[50:51], v[212:213], v[66:67] op_sel:[1,1] op_sel_hi:[0,1] neg_lo:[0,1]
	v_pk_fma_f32 v[30:31], v[212:213], v[66:67], v[50:51] op_sel_hi:[1,0,1]
	v_add_u32_e32 v50, 0xc00, v16
	v_ashrrev_i32_e32 v51, 31, v50
	v_lshl_add_u64 v[50:51], v[50:51], 3, s[46:47]
	s_nop 0
	v_pk_mul_f32 v[66:67], v[32:33], v[214:215] op_sel:[1,1] op_sel_hi:[1,0] neg_lo:[1,0]
	v_pk_fma_f32 v[32:33], v[32:33], v[214:215], v[66:67] op_sel_hi:[0,1,1]
	v_add_u32_e32 v50, 0xe00, v16
	v_ashrrev_i32_e32 v51, 31, v50
	v_lshl_add_u64 v[50:51], v[50:51], 3, s[46:47]
	s_nop 0
	v_pk_mul_f32 v[66:67], v[216:217], v[34:35] op_sel:[1,1] op_sel_hi:[0,1] neg_lo:[0,1]
	v_pk_fma_f32 v[34:35], v[216:217], v[34:35], v[66:67] op_sel_hi:[1,0,1]
	v_add_u32_e32 v50, 0x1000, v16
	v_ashrrev_i32_e32 v51, 31, v50
	v_lshl_add_u64 v[50:51], v[50:51], 3, s[46:47]
	s_nop 0
	v_pk_mul_f32 v[66:67], v[36:37], v[218:219] op_sel:[1,1] op_sel_hi:[1,0] neg_lo:[1,0]
	v_pk_fma_f32 v[36:37], v[36:37], v[218:219], v[66:67] op_sel_hi:[0,1,1]
	v_add_u32_e32 v50, 0x1200, v16
	v_ashrrev_i32_e32 v51, 31, v50
	v_lshl_add_u64 v[50:51], v[50:51], 3, s[46:47]
	v_pk_add_f32 v[70:71], v[20:21], v[36:37]
	v_pk_add_f32 v[20:21], v[20:21], v[36:37] neg_lo:[0,1] neg_hi:[0,1]
	s_nop 0
	v_pk_mul_f32 v[66:67], v[40:41], v[220:221] op_sel:[1,1] op_sel_hi:[1,0] neg_lo:[1,0]
	v_pk_fma_f32 v[40:41], v[40:41], v[220:221], v[66:67] op_sel_hi:[0,1,1]
	v_add_u32_e32 v50, 0x1400, v16
	v_ashrrev_i32_e32 v51, 31, v50
	v_lshl_add_u64 v[50:51], v[50:51], 3, s[46:47]
	v_pk_add_f32 v[36:37], v[22:23], v[40:41]
	v_pk_add_f32 v[22:23], v[22:23], v[40:41] neg_lo:[0,1] neg_hi:[0,1]
	s_nop 0
	v_pk_mul_f32 v[66:67], v[42:43], v[222:223] op_sel:[1,1] op_sel_hi:[1,0] neg_lo:[1,0]
	v_pk_fma_f32 v[42:43], v[42:43], v[222:223], v[66:67] op_sel_hi:[0,1,1]
	v_add_u32_e32 v50, 0x1600, v16
	v_ashrrev_i32_e32 v51, 31, v50
	v_lshl_add_u64 v[50:51], v[50:51], 3, s[46:47]
	s_nop 0
	v_pk_mul_f32 v[66:67], v[46:47], v[224:225] op_sel:[1,1] op_sel_hi:[1,0] neg_lo:[1,0]
	v_pk_fma_f32 v[46:47], v[46:47], v[224:225], v[66:67] op_sel_hi:[0,1,1]
	v_add_u32_e32 v50, 0x1800, v16
	v_ashrrev_i32_e32 v51, 31, v50
	v_lshl_add_u64 v[50:51], v[50:51], 3, s[46:47]
	s_nop 0
	v_pk_mul_f32 v[66:67], v[44:45], v[226:227] op_sel:[1,1] op_sel_hi:[1,0] neg_lo:[1,0]
	v_pk_fma_f32 v[44:45], v[44:45], v[226:227], v[66:67] op_sel_hi:[0,1,1]
	v_add_u32_e32 v50, 0x1a00, v16
	v_ashrrev_i32_e32 v51, 31, v50
	v_lshl_add_u64 v[50:51], v[50:51], 3, s[46:47]
	s_nop 0
	v_pk_mul_f32 v[66:67], v[48:49], v[228:229] op_sel:[1,1] op_sel_hi:[1,0] neg_lo:[1,0]
	v_pk_fma_f32 v[48:49], v[48:49], v[228:229], v[66:67] op_sel_hi:[0,1,1]
	v_add_u32_e32 v50, 0x1c00, v16
	v_ashrrev_i32_e32 v51, 31, v50
	v_lshl_add_u64 v[50:51], v[50:51], 3, s[46:47]
	s_nop 0
	v_pk_mul_f32 v[66:67], v[38:39], v[230:231] op_sel:[1,1] op_sel_hi:[1,0] neg_lo:[1,0]
	v_pk_fma_f32 v[38:39], v[38:39], v[230:231], v[66:67] op_sel_hi:[0,1,1]
	v_add_u32_e32 v50, 0x1e00, v16
	v_ashrrev_i32_e32 v51, 31, v50
	v_lshl_add_u64 v[50:51], v[50:51], 3, s[46:47]
	v_mov_b32_e32 v50, v232
	v_mov_b32_e32 v51, v233
	v_lshlrev_b32_e32 v190, 3, v16
	v_add_u32_e32 v190, 0x11000, v190
	global_load_dwordx2 v[202:203], v190, s[46:47] offset:-4096
	global_load_dwordx2 v[204:205], v190, s[46:47]
	v_add_u32_e32 v190, 0x2000, v190
	global_load_dwordx2 v[206:207], v190, s[46:47] offset:-4096
	global_load_dwordx2 v[208:209], v190, s[46:47]
	v_add_u32_e32 v190, 0x2000, v190
	global_load_dwordx2 v[210:211], v190, s[46:47] offset:-4096
	global_load_dwordx2 v[212:213], v190, s[46:47]
	v_add_u32_e32 v190, 0x2000, v190
	global_load_dwordx2 v[214:215], v190, s[46:47] offset:-4096
	global_load_dwordx2 v[216:217], v190, s[46:47]
	v_add_u32_e32 v190, 0x2000, v190
	global_load_dwordx2 v[218:219], v190, s[46:47] offset:-4096
	global_load_dwordx2 v[220:221], v190, s[46:47]
	v_add_u32_e32 v190, 0x2000, v190
	global_load_dwordx2 v[222:223], v190, s[46:47] offset:-4096
	global_load_dwordx2 v[224:225], v190, s[46:47]
	v_add_u32_e32 v190, 0x2000, v190
	global_load_dwordx2 v[226:227], v190, s[46:47] offset:-4096
	global_load_dwordx2 v[228:229], v190, s[46:47]
	v_add_u32_e32 v190, 0x2000, v190
	global_load_dwordx2 v[230:231], v190, s[46:47] offset:-4096
	global_load_dwordx2 v[232:233], v190, s[46:47]
	v_mov_b32_e32 v17, v164
	s_nop 0
	v_pk_mul_f32 v[66:67], v[18:19], v[50:51] op_sel:[1,1] op_sel_hi:[1,0] neg_lo:[1,0]
	v_pk_fma_f32 v[18:19], v[18:19], v[50:51], v[66:67] op_sel_hi:[0,1,1]
	v_mov_b32_e32 v50, v165
	v_mov_b32_e32 v17, v166
	v_mov_b32_e32 v66, v167
	v_mov_b32_e32 v17, v168
	s_nop 0
	v_pk_mul_f32 v[40:41], v[22:23], v[68:69] op_sel:[1,0] op_sel_hi:[0,0] neg_lo:[1,0]
	v_mov_b32_e32 v17, v170
	v_pk_fma_f32 v[22:23], v[22:23], v[50:51], v[40:41] op_sel_hi:[1,0,1]
	v_pk_add_f32 v[40:41], v[24:25], v[42:43]
	v_pk_add_f32 v[24:25], v[24:25], v[42:43] neg_lo:[0,1] neg_hi:[0,1]
	v_pk_mul_f32 v[42:43], v[24:25], v[66:67] op_sel:[1,0] op_sel_hi:[0,0] neg_lo:[1,0]
	v_mov_b32_e32 v17, v171
	v_pk_fma_f32 v[24:25], v[24:25], v[66:67], v[42:43] op_sel_hi:[1,0,1]
	v_pk_add_f32 v[42:43], v[26:27], v[46:47]
	v_pk_add_f32 v[26:27], v[26:27], v[46:47] neg_lo:[0,1] neg_hi:[0,1]
	v_pk_mul_f32 v[46:47], v[26:27], v[68:69] op_sel_hi:[1,0]
	v_pk_fma_f32 v[26:27], v[26:27], v[50:51], v[46:47] op_sel:[1,0,0] op_sel_hi:[0,0,1] neg_lo:[1,0,0]
	v_pk_add_f32 v[46:47], v[28:29], v[44:45]
	v_pk_add_f32 v[28:29], v[28:29], v[44:45] neg_lo:[0,1] neg_hi:[0,1]
	v_mov_b32_e32 v17, v175
	v_xor_b32_e32 v44, 0x80000000, v29
	v_mov_b32_e32 v45, v28
	v_pk_add_f32 v[28:29], v[30:31], v[48:49]
	v_pk_add_f32 v[30:31], v[30:31], v[48:49] neg_lo:[0,1] neg_hi:[0,1]
	v_pk_mul_f32 v[48:49], v[30:31], v[68:69] op_sel_hi:[1,0] neg_lo:[0,1] neg_hi:[0,1]
	v_pk_fma_f32 v[30:31], v[30:31], v[50:51], v[48:49] op_sel:[1,0,0] op_sel_hi:[0,0,1] neg_lo:[1,0,0]
	v_pk_add_f32 v[48:49], v[32:33], v[38:39]
	v_pk_add_f32 v[32:33], v[32:33], v[38:39] neg_lo:[0,1] neg_hi:[0,1]
	v_pk_mul_f32 v[38:39], v[32:33], v[66:67] op_sel:[1,0] op_sel_hi:[0,0] neg_lo:[1,0]
	v_pk_fma_f32 v[32:33], v[32:33], v[66:67], v[38:39] op_sel_hi:[1,0,1] neg_lo:[0,1,0] neg_hi:[0,1,0]
	v_pk_add_f32 v[38:39], v[34:35], v[18:19]
	v_pk_add_f32 v[18:19], v[34:35], v[18:19] neg_lo:[0,1] neg_hi:[0,1]
	v_pk_mul_f32 v[34:35], v[18:19], v[68:69] op_sel:[1,0] op_sel_hi:[0,0] neg_lo:[1,0]
	v_mov_b32_e32 v68, v169
	v_pk_fma_f32 v[18:19], v[18:19], v[50:51], v[34:35] op_sel_hi:[1,0,1] neg_lo:[0,1,0] neg_hi:[0,1,0]
	v_pk_add_f32 v[50:51], v[36:37], v[28:29]
	v_pk_add_f32 v[28:29], v[36:37], v[28:29] neg_lo:[0,1] neg_hi:[0,1]
	v_pk_add_f32 v[34:35], v[70:71], v[46:47]
	v_pk_mul_f32 v[36:37], v[28:29], v[66:67] op_sel:[1,0] op_sel_hi:[0,0] neg_lo:[1,0]
	v_pk_add_f32 v[46:47], v[70:71], v[46:47] neg_lo:[0,1] neg_hi:[0,1]
	v_pk_fma_f32 v[28:29], v[28:29], v[66:67], v[36:37] op_sel_hi:[1,0,1]
	v_pk_add_f32 v[36:37], v[40:41], v[48:49]
	v_pk_add_f32 v[40:41], v[40:41], v[48:49] neg_lo:[0,1] neg_hi:[0,1]
	v_xor_b32_e32 v48, 0x80000000, v41
	v_mov_b32_e32 v49, v40
	v_pk_add_f32 v[40:41], v[42:43], v[38:39]
	v_pk_add_f32 v[38:39], v[42:43], v[38:39] neg_lo:[0,1] neg_hi:[0,1]
	v_pk_mul_f32 v[42:43], v[66:67], v[38:39] op_sel:[0,1] op_sel_hi:[0,0] neg_lo:[0,1]
	v_pk_fma_f32 v[38:39], v[38:39], v[66:67], v[42:43] op_sel_hi:[1,0,1] neg_lo:[0,1,0] neg_hi:[0,1,0]
	v_pk_add_f32 v[42:43], v[34:35], v[36:37]
	v_pk_add_f32 v[34:35], v[34:35], v[36:37] neg_lo:[0,1] neg_hi:[0,1]
	v_pk_add_f32 v[36:37], v[50:51], v[40:41]
	v_pk_add_f32 v[40:41], v[50:51], v[40:41] neg_lo:[0,1] neg_hi:[0,1]
	v_xor_b32_e32 v50, 0x80000000, v41
	v_mov_b32_e32 v51, v40
	v_pk_add_f32 v[40:41], v[42:43], v[36:37]
	v_pk_add_f32 v[36:37], v[42:43], v[36:37] neg_lo:[0,1] neg_hi:[0,1]
	v_pk_add_f32 v[42:43], v[34:35], v[50:51]
	v_pk_add_f32 v[34:35], v[34:35], v[50:51] neg_lo:[0,1] neg_hi:[0,1]
	v_pk_add_f32 v[50:51], v[46:47], v[48:49]
	v_pk_add_f32 v[46:47], v[46:47], v[48:49] neg_lo:[0,1] neg_hi:[0,1]
	v_pk_add_f32 v[48:49], v[28:29], v[38:39]
	v_pk_add_f32 v[28:29], v[28:29], v[38:39] neg_lo:[0,1] neg_hi:[0,1]
	v_xor_b32_e32 v38, 0x80000000, v29
	v_mov_b32_e32 v39, v28
	v_pk_add_f32 v[28:29], v[50:51], v[48:49]
	v_pk_add_f32 v[48:49], v[50:51], v[48:49] neg_lo:[0,1] neg_hi:[0,1]
	v_pk_add_f32 v[50:51], v[46:47], v[38:39]
	v_pk_add_f32 v[38:39], v[46:47], v[38:39] neg_lo:[0,1] neg_hi:[0,1]
	v_pk_add_f32 v[46:47], v[20:21], v[44:45]
	v_pk_add_f32 v[20:21], v[20:21], v[44:45] neg_lo:[0,1] neg_hi:[0,1]
	v_pk_add_f32 v[44:45], v[22:23], v[30:31]
	v_pk_add_f32 v[22:23], v[22:23], v[30:31] neg_lo:[0,1] neg_hi:[0,1]
	v_pk_mul_f32 v[30:31], v[66:67], v[22:23] op_sel:[0,1] op_sel_hi:[0,0] neg_lo:[0,1]
	v_pk_fma_f32 v[22:23], v[66:67], v[22:23], v[30:31] op_sel_hi:[0,1,1]
	v_pk_add_f32 v[30:31], v[24:25], v[32:33]
	v_pk_add_f32 v[24:25], v[24:25], v[32:33] neg_lo:[0,1] neg_hi:[0,1]
	v_xor_b32_e32 v32, 0x80000000, v25
	v_mov_b32_e32 v33, v24
	v_pk_add_f32 v[24:25], v[26:27], v[18:19]
	v_pk_add_f32 v[18:19], v[26:27], v[18:19] neg_lo:[0,1] neg_hi:[0,1]
	v_pk_mul_f32 v[26:27], v[66:67], v[18:19] op_sel:[0,1] op_sel_hi:[0,0] neg_lo:[0,1]
	v_pk_fma_f32 v[18:19], v[66:67], v[18:19], v[26:27] op_sel_hi:[0,1,1] neg_lo:[1,0,0] neg_hi:[1,0,0]
	v_pk_add_f32 v[26:27], v[46:47], v[30:31]
	v_pk_add_f32 v[30:31], v[46:47], v[30:31] neg_lo:[0,1] neg_hi:[0,1]
	v_pk_add_f32 v[46:47], v[44:45], v[24:25]
	v_pk_add_f32 v[24:25], v[44:45], v[24:25] neg_lo:[0,1] neg_hi:[0,1]
	v_mov_b32_e32 v66, v167
	v_xor_b32_e32 v44, 0x80000000, v25
	v_mov_b32_e32 v45, v24
	v_pk_add_f32 v[24:25], v[26:27], v[46:47]
	v_pk_add_f32 v[26:27], v[26:27], v[46:47] neg_lo:[0,1] neg_hi:[0,1]
	v_pk_add_f32 v[46:47], v[30:31], v[44:45]
	v_pk_add_f32 v[30:31], v[30:31], v[44:45] neg_lo:[0,1] neg_hi:[0,1]
	v_pk_add_f32 v[44:45], v[20:21], v[32:33]
	v_pk_add_f32 v[20:21], v[20:21], v[32:33] neg_lo:[0,1] neg_hi:[0,1]
	v_pk_add_f32 v[32:33], v[22:23], v[18:19]
	v_pk_add_f32 v[18:19], v[22:23], v[18:19] neg_lo:[0,1] neg_hi:[0,1]
	v_xor_b32_e32 v22, 0x80000000, v19
	v_mov_b32_e32 v23, v18
	v_pk_add_f32 v[18:19], v[44:45], v[32:33]
	v_pk_add_f32 v[32:33], v[44:45], v[32:33] neg_lo:[0,1] neg_hi:[0,1]
	v_pk_add_f32 v[44:45], v[20:21], v[22:23]
	v_pk_add_f32 v[20:21], v[20:21], v[22:23] neg_lo:[0,1] neg_hi:[0,1]
	ds_write_b64 v10, v[40:41]
	ds_write_b64 v13, v[24:25]
	ds_write_b64 v15, v[28:29]
	ds_write_b64 v52, v[18:19]
	ds_write_b64 v53, v[42:43]
	ds_write_b64 v54, v[46:47]
	ds_write_b64 v55, v[50:51]
	ds_write_b64 v56, v[44:45]
	ds_write_b64 v57, v[36:37]
	ds_write_b64 v58, v[26:27]
	ds_write_b64 v59, v[48:49]
	ds_write_b64 v60, v[32:33]
	ds_write_b64 v61, v[34:35]
	ds_write_b64 v62, v[30:31]
	ds_write_b64 v63, v[38:39]
	ds_write_b64 v64, v[20:21]
	v_mov_b32_e32 v10, v177
	v_mov_b32_e32 v64, v165
	v_lshlrev_b32_e32 v13, 3, v17
	v_lshlrev_b32_e32 v48, 3, v10
	v_add3_u32 v10, 0, v13, v48
	v_xor_b32_e32 v13, 1, v17
	v_xor_b32_e32 v34, 8, v17
	v_xor_b32_e32 v36, 9, v17
	v_lshlrev_b32_e32 v13, 3, v13
	v_xor_b32_e32 v15, 2, v17
	v_xor_b32_e32 v24, 3, v17
	v_xor_b32_e32 v26, 4, v17
	v_xor_b32_e32 v28, 5, v17
	v_xor_b32_e32 v30, 6, v17
	v_xor_b32_e32 v32, 7, v17
	v_lshlrev_b32_e32 v34, 3, v34
	v_lshlrev_b32_e32 v36, 3, v36
	v_xor_b32_e32 v38, 10, v17
	v_xor_b32_e32 v40, 11, v17
	v_xor_b32_e32 v42, 12, v17
	v_xor_b32_e32 v44, 13, v17
	v_xor_b32_e32 v46, 14, v17
	v_xor_b32_e32 v17, 15, v17
	v_add3_u32 v13, 0, v13, v48
	v_lshlrev_b32_e32 v15, 3, v15
	v_lshlrev_b32_e32 v24, 3, v24
	v_lshlrev_b32_e32 v26, 3, v26
	v_lshlrev_b32_e32 v28, 3, v28
	v_lshlrev_b32_e32 v30, 3, v30
	v_lshlrev_b32_e32 v32, 3, v32
	v_add3_u32 v55, 0, v34, v48
	v_add3_u32 v56, 0, v36, v48
	v_lshlrev_b32_e32 v38, 3, v38
	v_lshlrev_b32_e32 v40, 3, v40
	v_lshlrev_b32_e32 v42, 3, v42
	v_lshlrev_b32_e32 v44, 3, v44
	v_lshlrev_b32_e32 v46, 3, v46
	v_lshlrev_b32_e32 v17, 3, v17
	ds_read_b64 v[18:19], v10
	ds_read_b64 v[20:21], v13
	v_add3_u32 v15, 0, v15, v48
	v_add3_u32 v50, 0, v24, v48
	v_add3_u32 v51, 0, v26, v48
	v_add3_u32 v52, 0, v28, v48
	v_add3_u32 v53, 0, v30, v48
	v_add3_u32 v54, 0, v32, v48
	ds_read_b64 v[34:35], v55
	ds_read_b64 v[36:37], v56
	v_add3_u32 v57, 0, v38, v48
	v_add3_u32 v58, 0, v40, v48
	v_add3_u32 v59, 0, v42, v48
	v_add3_u32 v60, 0, v44, v48
	v_add3_u32 v61, 0, v46, v48
	v_add3_u32 v62, 0, v17, v48
	v_mov_b32_e32 v17, v1
	ds_read_b64 v[22:23], v15
	ds_read_b64 v[24:25], v50
	ds_read_b64 v[26:27], v51
	ds_read_b64 v[28:29], v52
	ds_read_b64 v[30:31], v53
	ds_read_b64 v[32:33], v54
	ds_read_b64 v[38:39], v57
	ds_read_b64 v[40:41], v58
	ds_read_b64 v[42:43], v59
	ds_read_b64 v[44:45], v60
	ds_read_b64 v[46:47], v61
	ds_read_b64 v[48:49], v62
	s_waitcnt lgkmcnt(13)
	v_pk_add_f32 v[70:71], v[18:19], v[34:35]
	v_mov_b32_e32 v17, v164
	v_pk_add_f32 v[18:19], v[18:19], v[34:35] neg_lo:[0,1] neg_hi:[0,1]
	v_mov_b32_e32 v17, v166
	s_waitcnt lgkmcnt(12)
	v_pk_add_f32 v[34:35], v[20:21], v[36:37]
	v_pk_add_f32 v[20:21], v[20:21], v[36:37] neg_lo:[0,1] neg_hi:[0,1]
	v_mov_b32_e32 v17, v168
	s_nop 0
	v_pk_mul_f32 v[36:37], v[20:21], v[68:69] op_sel:[1,0] op_sel_hi:[0,0] neg_lo:[1,1] neg_hi:[0,1]
	v_mov_b32_e32 v17, v170
	v_pk_fma_f32 v[20:21], v[20:21], v[64:65], v[36:37] op_sel_hi:[1,0,1]
	s_waitcnt lgkmcnt(5)
	v_pk_add_f32 v[36:37], v[22:23], v[38:39]
	v_pk_add_f32 v[22:23], v[22:23], v[38:39] neg_lo:[0,1] neg_hi:[0,1]
	v_pk_mul_f32 v[38:39], v[22:23], v[66:67] op_sel:[1,0] op_sel_hi:[0,0] neg_lo:[1,1] neg_hi:[0,1]
	v_mov_b32_e32 v17, v171
	v_pk_fma_f32 v[22:23], v[22:23], v[66:67], v[38:39] op_sel_hi:[1,0,1]
	s_waitcnt lgkmcnt(4)
	v_pk_add_f32 v[38:39], v[24:25], v[40:41]
	v_pk_add_f32 v[24:25], v[24:25], v[40:41] neg_lo:[0,1] neg_hi:[0,1]
	v_pk_mul_f32 v[40:41], v[24:25], v[68:69] op_sel_hi:[1,0]
	v_pk_fma_f32 v[24:25], v[24:25], v[64:65], v[40:41] op_sel:[1,0,0] op_sel_hi:[0,0,1] neg_lo:[1,1,0] neg_hi:[0,1,0]
	s_waitcnt lgkmcnt(3)
	v_pk_add_f32 v[40:41], v[26:27], v[42:43]
	v_pk_add_f32 v[26:27], v[26:27], v[42:43] neg_lo:[0,1] neg_hi:[0,1]
	v_xor_b32_e32 v73, 0x80000000, v26
	v_mov_b32_e32 v72, v27
	s_waitcnt lgkmcnt(2)
	v_pk_add_f32 v[26:27], v[28:29], v[44:45]
	v_pk_add_f32 v[28:29], v[28:29], v[44:45] neg_lo:[0,1] neg_hi:[0,1]
	v_pk_mul_f32 v[42:43], v[28:29], v[68:69] op_sel_hi:[1,0] neg_lo:[0,1] neg_hi:[0,1]
	v_pk_fma_f32 v[28:29], v[28:29], v[64:65], v[42:43] op_sel:[1,0,0] op_sel_hi:[0,0,1] neg_lo:[1,1,0] neg_hi:[0,1,0]
	s_waitcnt lgkmcnt(1)
	v_pk_add_f32 v[42:43], v[30:31], v[46:47]
	v_pk_add_f32 v[30:31], v[30:31], v[46:47] neg_lo:[0,1] neg_hi:[0,1]
	v_pk_mul_f32 v[44:45], v[30:31], v[66:67] op_sel:[1,0] op_sel_hi:[0,0] neg_lo:[1,1] neg_hi:[0,1]
	v_pk_fma_f32 v[30:31], v[30:31], v[66:67], v[44:45] op_sel_hi:[1,0,1] neg_lo:[0,1,0] neg_hi:[0,1,0]
	s_waitcnt lgkmcnt(0)
	v_pk_add_f32 v[44:45], v[32:33], v[48:49]
	v_pk_add_f32 v[32:33], v[32:33], v[48:49] neg_lo:[0,1] neg_hi:[0,1]
	v_pk_add_f32 v[48:49], v[34:35], v[26:27]
	v_pk_add_f32 v[26:27], v[34:35], v[26:27] neg_lo:[0,1] neg_hi:[0,1]
	v_pk_mul_f32 v[34:35], v[26:27], v[66:67] op_sel:[1,0] op_sel_hi:[0,0] neg_lo:[1,1] neg_hi:[0,1]
	v_pk_fma_f32 v[26:27], v[26:27], v[66:67], v[34:35] op_sel_hi:[1,0,1]
	v_pk_add_f32 v[34:35], v[36:37], v[42:43]
	v_pk_add_f32 v[36:37], v[36:37], v[42:43] neg_lo:[0,1] neg_hi:[0,1]
	v_pk_mul_f32 v[46:47], v[32:33], v[68:69] op_sel:[1,0] op_sel_hi:[0,0] neg_lo:[1,1] neg_hi:[0,1]
	v_xor_b32_e32 v43, 0x80000000, v36
	v_mov_b32_e32 v42, v37
	v_pk_add_f32 v[36:37], v[38:39], v[44:45]
	v_pk_add_f32 v[38:39], v[38:39], v[44:45] neg_lo:[0,1] neg_hi:[0,1]
	v_pk_fma_f32 v[46:47], v[32:33], v[64:65], v[46:47] op_sel_hi:[1,0,1] neg_lo:[0,1,0] neg_hi:[0,1,0]
	v_pk_add_f32 v[32:33], v[70:71], v[40:41]
	v_pk_mul_f32 v[44:45], v[38:39], v[66:67] op_sel:[1,0] op_sel_hi:[0,0] neg_lo:[1,1] neg_hi:[0,1]
	v_pk_add_f32 v[40:41], v[70:71], v[40:41] neg_lo:[0,1] neg_hi:[0,1]
	v_pk_fma_f32 v[38:39], v[38:39], v[66:67], v[44:45] op_sel_hi:[1,0,1] neg_lo:[0,1,0] neg_hi:[0,1,0]
	v_pk_add_f32 v[44:45], v[32:33], v[34:35]
	v_pk_add_f32 v[32:33], v[32:33], v[34:35] neg_lo:[0,1] neg_hi:[0,1]
	v_pk_add_f32 v[34:35], v[48:49], v[36:37]
	v_pk_add_f32 v[36:37], v[48:49], v[36:37] neg_lo:[0,1] neg_hi:[0,1]
	v_pk_add_f32 v[64:65], v[44:45], v[34:35]
	v_xor_b32_e32 v49, 0x80000000, v36
	v_mov_b32_e32 v48, v37
	v_pk_add_f32 v[36:37], v[44:45], v[34:35] neg_lo:[0,1] neg_hi:[0,1]
	v_pk_add_f32 v[68:69], v[32:33], v[48:49]
	v_pk_add_f32 v[44:45], v[32:33], v[48:49] neg_lo:[0,1] neg_hi:[0,1]
	v_pk_add_f32 v[32:33], v[40:41], v[42:43]
	v_pk_add_f32 v[34:35], v[40:41], v[42:43] neg_lo:[0,1] neg_hi:[0,1]
	v_pk_add_f32 v[40:41], v[26:27], v[38:39]
	v_pk_add_f32 v[26:27], v[26:27], v[38:39] neg_lo:[0,1] neg_hi:[0,1]
	v_pk_add_f32 v[42:43], v[32:33], v[40:41] neg_lo:[0,1] neg_hi:[0,1]
	v_xor_b32_e32 v39, 0x80000000, v26
	v_mov_b32_e32 v38, v27
	v_pk_add_f32 v[26:27], v[32:33], v[40:41]
	v_pk_add_f32 v[40:41], v[20:21], v[28:29]
	v_pk_add_f32 v[20:21], v[20:21], v[28:29] neg_lo:[0,1] neg_hi:[0,1]
	v_pk_add_f32 v[32:33], v[34:35], v[38:39]
	v_pk_mul_f32 v[28:29], v[66:67], v[20:21] op_sel:[0,1] op_sel_hi:[0,0] neg_lo:[1,1] neg_hi:[1,0]
	v_pk_fma_f32 v[20:21], v[66:67], v[20:21], v[28:29] op_sel_hi:[0,1,1]
	v_pk_add_f32 v[28:29], v[22:23], v[30:31]
	v_pk_add_f32 v[22:23], v[22:23], v[30:31] neg_lo:[0,1] neg_hi:[0,1]
	v_pk_add_f32 v[38:39], v[34:35], v[38:39] neg_lo:[0,1] neg_hi:[0,1]
	v_xor_b32_e32 v31, 0x80000000, v22
	v_mov_b32_e32 v30, v23
	v_pk_add_f32 v[22:23], v[24:25], v[46:47]
	v_pk_add_f32 v[24:25], v[24:25], v[46:47] neg_lo:[0,1] neg_hi:[0,1]
	v_pk_add_f32 v[34:35], v[18:19], v[72:73]
	v_pk_mul_f32 v[46:47], v[66:67], v[24:25] op_sel:[0,1] op_sel_hi:[0,0] neg_lo:[1,1] neg_hi:[1,0]
	v_pk_fma_f32 v[24:25], v[66:67], v[24:25], v[46:47] op_sel_hi:[0,1,1] neg_lo:[1,0,0] neg_hi:[1,0,0]
	v_pk_add_f32 v[46:47], v[34:35], v[28:29]
	v_pk_add_f32 v[28:29], v[34:35], v[28:29] neg_lo:[0,1] neg_hi:[0,1]
	v_pk_add_f32 v[34:35], v[40:41], v[22:23]
	v_pk_add_f32 v[22:23], v[40:41], v[22:23] neg_lo:[0,1] neg_hi:[0,1]
	v_pk_add_f32 v[18:19], v[18:19], v[72:73] neg_lo:[0,1] neg_hi:[0,1]
	v_pk_add_f32 v[66:67], v[28:29], v[22:23] op_sel:[0,1] op_sel_hi:[1,0] neg_hi:[0,1]
	v_pk_add_f32 v[48:49], v[28:29], v[22:23] op_sel:[0,1] op_sel_hi:[1,0] neg_lo:[0,1]
	v_pk_add_f32 v[28:29], v[18:19], v[30:31]
	v_pk_add_f32 v[18:19], v[18:19], v[30:31] neg_lo:[0,1] neg_hi:[0,1]
	v_pk_add_f32 v[30:31], v[20:21], v[24:25]
	v_pk_add_f32 v[20:21], v[20:21], v[24:25] neg_lo:[0,1] neg_hi:[0,1]
	v_pk_add_f32 v[22:23], v[46:47], v[34:35]
	v_xor_b32_e32 v25, 0x80000000, v20
	v_add_u32_e32 v20, 0x2000, v16
	v_mov_b32_e32 v24, v21
	v_ashrrev_i32_e32 v21, 31, v20
	v_lshl_add_u64 v[20:21], v[20:21], 3, s[46:47]
	s_waitcnt vmcnt(0)
	v_pk_add_f32 v[40:41], v[46:47], v[34:35] neg_lo:[0,1] neg_hi:[0,1]
	v_pk_add_f32 v[34:35], v[18:19], v[24:25]
	v_pk_add_f32 v[18:19], v[18:19], v[24:25] neg_lo:[0,1] neg_hi:[0,1]
	v_pk_add_f32 v[70:71], v[28:29], v[30:31]
	v_pk_add_f32 v[46:47], v[28:29], v[30:31] neg_lo:[0,1] neg_hi:[0,1]
	s_nop 0
	v_pk_mul_f32 v[24:25], v[64:65], v[202:203] op_sel:[1,1] op_sel_hi:[1,0] neg_lo:[1,0]
	v_pk_fma_f32 v[20:21], v[64:65], v[202:203], v[24:25] op_sel_hi:[0,1,1]
	v_add_u32_e32 v24, 0x2200, v16
	v_ashrrev_i32_e32 v25, 31, v24
	v_lshl_add_u64 v[24:25], v[24:25], 3, s[46:47]
	s_nop 0
	v_pk_mul_f32 v[28:29], v[204:205], v[22:23] op_sel:[1,1] op_sel_hi:[0,1] neg_lo:[0,1]
	v_pk_fma_f32 v[22:23], v[204:205], v[22:23], v[28:29] op_sel_hi:[1,0,1]
	v_add_u32_e32 v24, 0x2400, v16
	v_ashrrev_i32_e32 v25, 31, v24
	v_lshl_add_u64 v[24:25], v[24:25], 3, s[46:47]
	s_nop 0
	v_pk_mul_f32 v[28:29], v[26:27], v[206:207] op_sel:[1,1] op_sel_hi:[1,0] neg_lo:[1,0]
	v_pk_fma_f32 v[24:25], v[26:27], v[206:207], v[28:29] op_sel_hi:[0,1,1]
	v_add_u32_e32 v26, 0x2600, v16
	v_ashrrev_i32_e32 v27, 31, v26
	v_lshl_add_u64 v[26:27], v[26:27], 3, s[46:47]
	s_nop 0
	v_pk_mul_f32 v[28:29], v[208:209], v[70:71] op_sel:[1,1] op_sel_hi:[0,1] neg_lo:[0,1]
	v_pk_fma_f32 v[26:27], v[208:209], v[70:71], v[28:29] op_sel_hi:[1,0,1]
	v_add_u32_e32 v28, 0x2800, v16
	v_ashrrev_i32_e32 v29, 31, v28
	v_lshl_add_u64 v[28:29], v[28:29], 3, s[46:47]
	s_nop 0
	v_pk_mul_f32 v[30:31], v[68:69], v[210:211] op_sel:[1,1] op_sel_hi:[1,0] neg_lo:[1,0]
	v_pk_fma_f32 v[28:29], v[68:69], v[210:211], v[30:31] op_sel_hi:[0,1,1]
	v_add_u32_e32 v30, 0x2a00, v16
	v_ashrrev_i32_e32 v31, 31, v30
	v_lshl_add_u64 v[30:31], v[30:31], 3, s[46:47]
	s_nop 0
	v_pk_mul_f32 v[64:65], v[212:213], v[66:67] op_sel:[1,1] op_sel_hi:[0,1] neg_lo:[0,1]
	v_pk_fma_f32 v[30:31], v[212:213], v[66:67], v[64:65] op_sel_hi:[1,0,1]
	v_add_u32_e32 v64, 0x2c00, v16
	v_ashrrev_i32_e32 v65, 31, v64
	v_lshl_add_u64 v[64:65], v[64:65], 3, s[46:47]
	s_nop 0
	v_pk_mul_f32 v[66:67], v[32:33], v[214:215] op_sel:[1,1] op_sel_hi:[1,0] neg_lo:[1,0]
	v_pk_fma_f32 v[32:33], v[32:33], v[214:215], v[66:67] op_sel_hi:[0,1,1]
	v_add_u32_e32 v64, 0x2e00, v16
	v_ashrrev_i32_e32 v65, 31, v64
	v_lshl_add_u64 v[64:65], v[64:65], 3, s[46:47]
	s_nop 0
	v_pk_mul_f32 v[66:67], v[216:217], v[34:35] op_sel:[1,1] op_sel_hi:[0,1] neg_lo:[0,1]
	v_pk_fma_f32 v[34:35], v[216:217], v[34:35], v[66:67] op_sel_hi:[1,0,1]
	v_add_u32_e32 v64, 0x3000, v16
	v_ashrrev_i32_e32 v65, 31, v64
	v_lshl_add_u64 v[64:65], v[64:65], 3, s[46:47]
	s_nop 0
	v_pk_mul_f32 v[66:67], v[36:37], v[218:219] op_sel:[1,1] op_sel_hi:[1,0] neg_lo:[1,0]
	v_pk_fma_f32 v[36:37], v[36:37], v[218:219], v[66:67] op_sel_hi:[0,1,1]
	v_add_u32_e32 v64, 0x3200, v16
	v_ashrrev_i32_e32 v65, 31, v64
	v_lshl_add_u64 v[64:65], v[64:65], 3, s[46:47]
	v_pk_add_f32 v[68:69], v[20:21], v[36:37]
	v_pk_add_f32 v[20:21], v[20:21], v[36:37] neg_lo:[0,1] neg_hi:[0,1]
	s_nop 0
	v_pk_mul_f32 v[66:67], v[40:41], v[220:221] op_sel:[1,1] op_sel_hi:[1,0] neg_lo:[1,0]
	v_pk_fma_f32 v[40:41], v[40:41], v[220:221], v[66:67] op_sel_hi:[0,1,1]
	v_add_u32_e32 v64, 0x3400, v16
	v_ashrrev_i32_e32 v65, 31, v64
	v_lshl_add_u64 v[64:65], v[64:65], 3, s[46:47]
	v_pk_add_f32 v[36:37], v[22:23], v[40:41]
	v_pk_add_f32 v[22:23], v[22:23], v[40:41] neg_lo:[0,1] neg_hi:[0,1]
	s_nop 0
	v_pk_mul_f32 v[66:67], v[42:43], v[222:223] op_sel:[1,1] op_sel_hi:[1,0] neg_lo:[1,0]
	v_pk_fma_f32 v[42:43], v[42:43], v[222:223], v[66:67] op_sel_hi:[0,1,1]
	v_add_u32_e32 v64, 0x3600, v16
	v_ashrrev_i32_e32 v65, 31, v64
	v_lshl_add_u64 v[64:65], v[64:65], 3, s[46:47]
	s_nop 0
	v_pk_mul_f32 v[66:67], v[46:47], v[224:225] op_sel:[1,1] op_sel_hi:[1,0] neg_lo:[1,0]
	v_pk_fma_f32 v[46:47], v[46:47], v[224:225], v[66:67] op_sel_hi:[0,1,1]
	v_add_u32_e32 v64, 0x3800, v16
	v_ashrrev_i32_e32 v65, 31, v64
	v_lshl_add_u64 v[64:65], v[64:65], 3, s[46:47]
	s_nop 0
	v_pk_mul_f32 v[66:67], v[44:45], v[226:227] op_sel:[1,1] op_sel_hi:[1,0] neg_lo:[1,0]
	v_pk_fma_f32 v[44:45], v[44:45], v[226:227], v[66:67] op_sel_hi:[0,1,1]
	v_add_u32_e32 v64, 0x3a00, v16
	v_ashrrev_i32_e32 v65, 31, v64
	v_lshl_add_u64 v[64:65], v[64:65], 3, s[46:47]
	s_nop 0
	v_pk_mul_f32 v[66:67], v[48:49], v[228:229] op_sel:[1,1] op_sel_hi:[1,0] neg_lo:[1,0]
	v_pk_fma_f32 v[48:49], v[48:49], v[228:229], v[66:67] op_sel_hi:[0,1,1]
	v_add_u32_e32 v64, 0x3c00, v16
	v_ashrrev_i32_e32 v65, 31, v64
	v_lshl_add_u64 v[64:65], v[64:65], 3, s[46:47]
	v_add_u32_e32 v16, 0x3e00, v16
	v_ashrrev_i32_e32 v17, 31, v16
	v_lshl_add_u64 v[16:17], v[16:17], 3, s[46:47]
	s_nop 0
	v_pk_mul_f32 v[66:67], v[38:39], v[230:231] op_sel:[1,1] op_sel_hi:[1,0] neg_lo:[1,0]
	v_pk_fma_f32 v[38:39], v[38:39], v[230:231], v[66:67] op_sel_hi:[0,1,1]
	s_nop 0
	v_pk_mul_f32 v[64:65], v[18:19], v[232:233] op_sel:[1,1] op_sel_hi:[1,0] neg_lo:[1,0]
	v_mov_b32_e32 v66, v169
	v_pk_fma_f32 v[16:17], v[18:19], v[232:233], v[64:65] op_sel_hi:[0,1,1]
	v_mov_b32_e32 v18, v1
	v_mov_b32_e32 v19, v166
	v_mov_b32_e32 v18, v164
	v_mov_b32_e32 v64, v167
	v_mov_b32_e32 v18, v165
	s_nop 0
	v_mov_b32_e32 v19, v168
	s_nop 0
	v_mov_b32_e32 v19, v170
	v_pk_mul_f32 v[40:41], v[22:23], v[66:67] op_sel:[1,0] op_sel_hi:[0,0] neg_lo:[1,0]
	v_mov_b32_e32 v19, v171
	s_nop 0
	v_pk_fma_f32 v[22:23], v[22:23], v[18:19], v[40:41] op_sel_hi:[1,0,1]
	v_pk_add_f32 v[40:41], v[24:25], v[42:43]
	v_pk_add_f32 v[24:25], v[24:25], v[42:43] neg_lo:[0,1] neg_hi:[0,1]
	v_pk_mul_f32 v[42:43], v[24:25], v[64:65] op_sel:[1,0] op_sel_hi:[0,0] neg_lo:[1,0]
	v_pk_fma_f32 v[24:25], v[24:25], v[64:65], v[42:43] op_sel_hi:[1,0,1]
	v_pk_add_f32 v[42:43], v[26:27], v[46:47]
	v_pk_add_f32 v[26:27], v[26:27], v[46:47] neg_lo:[0,1] neg_hi:[0,1]
	v_pk_mul_f32 v[46:47], v[26:27], v[66:67] op_sel_hi:[1,0]
	v_pk_fma_f32 v[26:27], v[26:27], v[18:19], v[46:47] op_sel:[1,0,0] op_sel_hi:[0,0,1] neg_lo:[1,0,0]
	v_pk_add_f32 v[46:47], v[28:29], v[44:45]
	v_pk_add_f32 v[28:29], v[28:29], v[44:45] neg_lo:[0,1] neg_hi:[0,1]
	v_xor_b32_e32 v44, 0x80000000, v29
	v_mov_b32_e32 v45, v28
	v_pk_add_f32 v[28:29], v[30:31], v[48:49]
	v_pk_add_f32 v[30:31], v[30:31], v[48:49] neg_lo:[0,1] neg_hi:[0,1]
	v_pk_mul_f32 v[48:49], v[30:31], v[66:67] op_sel_hi:[1,0] neg_lo:[0,1] neg_hi:[0,1]
	v_pk_fma_f32 v[30:31], v[30:31], v[18:19], v[48:49] op_sel:[1,0,0] op_sel_hi:[0,0,1] neg_lo:[1,0,0]
	v_pk_add_f32 v[48:49], v[32:33], v[38:39]
	v_pk_add_f32 v[32:33], v[32:33], v[38:39] neg_lo:[0,1] neg_hi:[0,1]
	v_pk_mul_f32 v[38:39], v[32:33], v[64:65] op_sel:[1,0] op_sel_hi:[0,0] neg_lo:[1,0]
	v_pk_fma_f32 v[32:33], v[32:33], v[64:65], v[38:39] op_sel_hi:[1,0,1] neg_lo:[0,1,0] neg_hi:[0,1,0]
	v_pk_add_f32 v[38:39], v[34:35], v[16:17]
	v_pk_add_f32 v[16:17], v[34:35], v[16:17] neg_lo:[0,1] neg_hi:[0,1]
	v_pk_mul_f32 v[34:35], v[16:17], v[66:67] op_sel:[1,0] op_sel_hi:[0,0] neg_lo:[1,0]
	v_pk_fma_f32 v[16:17], v[16:17], v[18:19], v[34:35] op_sel_hi:[1,0,1] neg_lo:[0,1,0] neg_hi:[0,1,0]
	v_pk_add_f32 v[18:19], v[68:69], v[46:47]
	v_pk_add_f32 v[34:35], v[68:69], v[46:47] neg_lo:[0,1] neg_hi:[0,1]
	v_pk_add_f32 v[46:47], v[36:37], v[28:29]
	v_pk_add_f32 v[28:29], v[36:37], v[28:29] neg_lo:[0,1] neg_hi:[0,1]
	v_pk_mul_f32 v[36:37], v[28:29], v[64:65] op_sel:[1,0] op_sel_hi:[0,0] neg_lo:[1,0]
	v_pk_fma_f32 v[28:29], v[28:29], v[64:65], v[36:37] op_sel_hi:[1,0,1]
	v_pk_add_f32 v[36:37], v[40:41], v[48:49]
	v_pk_add_f32 v[40:41], v[40:41], v[48:49] neg_lo:[0,1] neg_hi:[0,1]
	v_xor_b32_e32 v48, 0x80000000, v41
	v_mov_b32_e32 v49, v40
	v_pk_add_f32 v[40:41], v[42:43], v[38:39]
	v_pk_add_f32 v[38:39], v[42:43], v[38:39] neg_lo:[0,1] neg_hi:[0,1]
	v_pk_mul_f32 v[42:43], v[64:65], v[38:39] op_sel:[0,1] op_sel_hi:[0,0] neg_lo:[0,1]
	v_pk_fma_f32 v[38:39], v[38:39], v[64:65], v[42:43] op_sel_hi:[1,0,1] neg_lo:[0,1,0] neg_hi:[0,1,0]
	v_pk_add_f32 v[42:43], v[18:19], v[36:37]
	v_pk_add_f32 v[18:19], v[18:19], v[36:37] neg_lo:[0,1] neg_hi:[0,1]
	v_pk_add_f32 v[36:37], v[46:47], v[40:41]
	v_pk_add_f32 v[40:41], v[46:47], v[40:41] neg_lo:[0,1] neg_hi:[0,1]
	v_xor_b32_e32 v46, 0x80000000, v41
	v_mov_b32_e32 v47, v40
	v_pk_add_f32 v[40:41], v[42:43], v[36:37]
	v_pk_add_f32 v[36:37], v[42:43], v[36:37] neg_lo:[0,1] neg_hi:[0,1]
	v_pk_add_f32 v[42:43], v[18:19], v[46:47]
	v_pk_add_f32 v[18:19], v[18:19], v[46:47] neg_lo:[0,1] neg_hi:[0,1]
	v_pk_add_f32 v[46:47], v[34:35], v[48:49]
	v_pk_add_f32 v[34:35], v[34:35], v[48:49] neg_lo:[0,1] neg_hi:[0,1]
	v_pk_add_f32 v[48:49], v[28:29], v[38:39]
	v_pk_add_f32 v[28:29], v[28:29], v[38:39] neg_lo:[0,1] neg_hi:[0,1]
	v_xor_b32_e32 v38, 0x80000000, v29
	v_mov_b32_e32 v39, v28
	v_pk_add_f32 v[28:29], v[46:47], v[48:49]
	v_pk_add_f32 v[46:47], v[46:47], v[48:49] neg_lo:[0,1] neg_hi:[0,1]
	v_pk_add_f32 v[48:49], v[34:35], v[38:39]
	v_pk_add_f32 v[34:35], v[34:35], v[38:39] neg_lo:[0,1] neg_hi:[0,1]
	v_pk_add_f32 v[38:39], v[20:21], v[44:45]
	v_pk_add_f32 v[20:21], v[20:21], v[44:45] neg_lo:[0,1] neg_hi:[0,1]
	v_pk_add_f32 v[44:45], v[22:23], v[30:31]
	v_pk_add_f32 v[22:23], v[22:23], v[30:31] neg_lo:[0,1] neg_hi:[0,1]
	v_pk_mul_f32 v[30:31], v[64:65], v[22:23] op_sel:[0,1] op_sel_hi:[0,0] neg_lo:[0,1]
	v_pk_fma_f32 v[22:23], v[64:65], v[22:23], v[30:31] op_sel_hi:[0,1,1]
	v_pk_add_f32 v[30:31], v[24:25], v[32:33]
	v_pk_add_f32 v[24:25], v[24:25], v[32:33] neg_lo:[0,1] neg_hi:[0,1]
	v_xor_b32_e32 v32, 0x80000000, v25
	v_mov_b32_e32 v33, v24
	v_pk_add_f32 v[24:25], v[26:27], v[16:17]
	v_pk_add_f32 v[16:17], v[26:27], v[16:17] neg_lo:[0,1] neg_hi:[0,1]
	v_pk_mul_f32 v[26:27], v[64:65], v[16:17] op_sel:[0,1] op_sel_hi:[0,0] neg_lo:[0,1]
	v_pk_fma_f32 v[16:17], v[64:65], v[16:17], v[26:27] op_sel_hi:[0,1,1] neg_lo:[1,0,0] neg_hi:[1,0,0]
	v_pk_add_f32 v[26:27], v[38:39], v[30:31]
	v_pk_add_f32 v[30:31], v[38:39], v[30:31] neg_lo:[0,1] neg_hi:[0,1]
	v_pk_add_f32 v[38:39], v[44:45], v[24:25]
	v_pk_add_f32 v[24:25], v[44:45], v[24:25] neg_lo:[0,1] neg_hi:[0,1]
	v_xor_b32_e32 v44, 0x80000000, v25
	v_mov_b32_e32 v45, v24
	v_pk_add_f32 v[24:25], v[26:27], v[38:39]
	v_pk_add_f32 v[26:27], v[26:27], v[38:39] neg_lo:[0,1] neg_hi:[0,1]
	v_pk_add_f32 v[38:39], v[30:31], v[44:45]
	v_pk_add_f32 v[30:31], v[30:31], v[44:45] neg_lo:[0,1] neg_hi:[0,1]
	v_pk_add_f32 v[44:45], v[20:21], v[32:33]
	v_pk_add_f32 v[20:21], v[20:21], v[32:33] neg_lo:[0,1] neg_hi:[0,1]
	v_pk_add_f32 v[32:33], v[22:23], v[16:17]
	v_pk_add_f32 v[16:17], v[22:23], v[16:17] neg_lo:[0,1] neg_hi:[0,1]
	v_xor_b32_e32 v22, 0x80000000, v17
	v_mov_b32_e32 v23, v16
	v_pk_add_f32 v[16:17], v[44:45], v[32:33]
	v_pk_add_f32 v[32:33], v[44:45], v[32:33] neg_lo:[0,1] neg_hi:[0,1]
	v_pk_add_f32 v[44:45], v[20:21], v[22:23]
	v_pk_add_f32 v[20:21], v[20:21], v[22:23] neg_lo:[0,1] neg_hi:[0,1]
	ds_write_b64 v10, v[40:41]
	ds_write_b64 v13, v[24:25]
	ds_write_b64 v15, v[28:29]
	ds_write_b64 v50, v[16:17]
	ds_write_b64 v51, v[42:43]
	ds_write_b64 v52, v[38:39]
	ds_write_b64 v53, v[48:49]
	ds_write_b64 v54, v[44:45]
	ds_write_b64 v55, v[36:37]
	ds_write_b64 v56, v[26:27]
	ds_write_b64 v57, v[46:47]
	ds_write_b64 v58, v[32:33]
	ds_write_b64 v59, v[18:19]
	ds_write_b64 v60, v[30:31]
	ds_write_b64 v61, v[34:35]
	ds_write_b64 v62, v[20:21]
	v_mov_b32_e32 v10, v174
	v_mov_b32_e32 v50, v172
	s_waitcnt lgkmcnt(0)
	s_barrier
	v_add_u32_e32 v13, v50, v10
	v_lshl_add_u32 v13, v13, 3, 0
	ds_read2_b64 v[16:19], v13 offset1:16
	v_xad_u32 v15, v50, 1, v10
	v_lshl_add_u32 v15, v15, 3, 0
	s_waitcnt lgkmcnt(0)
	v_pk_fma_f32 v[16:17], v[16:17], 0, v[16:17] op_sel:[1,0,0] op_sel_hi:[0,0,1] neg_hi:[1,0,0]
	v_pk_fma_f32 v[22:23], v[180:181], s[90:91], v[180:181] op_sel:[1,0,0] op_sel_hi:[0,1,1]
	v_pk_mul_f32 v[24:25], v[22:23], v[18:19] op_sel:[1,1] op_sel_hi:[1,0] neg_hi:[0,1]
	v_pk_fma_f32 v[18:19], v[18:19], v[22:23], v[24:25] op_sel_hi:[1,0,1]
	v_pk_mul_f32 v[24:25], v[180:181], v[22:23] op_sel:[1,1] op_sel_hi:[0,1] neg_lo:[0,1]
	v_pk_fma_f32 v[26:27], v[180:181], v[22:23], v[24:25] op_sel_hi:[1,0,1]
	ds_read2_b64 v[22:25], v15 offset0:32 offset1:48
	s_waitcnt lgkmcnt(0)
	v_pk_mul_f32 v[28:29], v[22:23], v[26:27] op_sel:[1,1] op_sel_hi:[0,1] neg_hi:[1,0]
	v_pk_fma_f32 v[22:23], v[22:23], v[26:27], v[28:29] op_sel_hi:[1,0,1]
	v_pk_mul_f32 v[28:29], v[180:181], v[26:27] op_sel:[1,1] op_sel_hi:[0,1] neg_lo:[0,1]
	v_pk_fma_f32 v[26:27], v[180:181], v[26:27], v[28:29] op_sel_hi:[1,0,1]
	v_pk_mul_f32 v[28:29], v[24:25], v[26:27] op_sel:[1,1] op_sel_hi:[0,1] neg_hi:[1,0]
	v_pk_fma_f32 v[24:25], v[24:25], v[26:27], v[28:29] op_sel_hi:[1,0,1]
	v_pk_mul_f32 v[28:29], v[180:181], v[26:27] op_sel:[1,1] op_sel_hi:[0,1] neg_lo:[0,1]
	v_pk_fma_f32 v[26:27], v[180:181], v[26:27], v[28:29] op_sel_hi:[1,0,1]
	v_xad_u32 v28, v50, 2, v10
	v_lshl_add_u32 v51, v28, 3, 0
	ds_read2_b64 v[28:31], v51 offset0:64 offset1:80
	v_pk_mul_f32 v[32:33], v[180:181], v[26:27] op_sel:[1,1] op_sel_hi:[0,1] neg_lo:[0,1]
	s_waitcnt lgkmcnt(0)
	v_pk_mul_f32 v[34:35], v[28:29], v[26:27] op_sel:[1,1] op_sel_hi:[0,1] neg_hi:[1,0]
	v_pk_fma_f32 v[28:29], v[28:29], v[26:27], v[34:35] op_sel_hi:[1,0,1]
	v_pk_fma_f32 v[34:35], v[180:181], v[26:27], v[32:33] op_sel_hi:[1,0,1]
	v_pk_mul_f32 v[26:27], v[30:31], v[34:35] op_sel:[1,1] op_sel_hi:[0,1] neg_hi:[1,0]
	v_pk_fma_f32 v[26:27], v[30:31], v[34:35], v[26:27] op_sel_hi:[1,0,1]
	v_xad_u32 v30, v50, 3, v10
	v_lshl_add_u32 v54, v30, 3, 0
	ds_read2_b64 v[30:33], v54 offset0:96 offset1:112
	v_pk_mul_f32 v[36:37], v[180:181], v[34:35] op_sel:[1,1] op_sel_hi:[0,1] neg_lo:[0,1]
	v_pk_fma_f32 v[34:35], v[180:181], v[34:35], v[36:37] op_sel_hi:[1,0,1]
	s_waitcnt lgkmcnt(0)
	v_pk_mul_f32 v[36:37], v[30:31], v[34:35] op_sel:[1,1] op_sel_hi:[0,1] neg_hi:[1,0]
	v_pk_fma_f32 v[30:31], v[30:31], v[34:35], v[36:37] op_sel_hi:[1,0,1]
	v_pk_mul_f32 v[36:37], v[180:181], v[34:35] op_sel:[1,1] op_sel_hi:[0,1] neg_lo:[0,1]
	v_pk_fma_f32 v[34:35], v[180:181], v[34:35], v[36:37] op_sel_hi:[1,0,1]
	v_pk_mul_f32 v[36:37], v[32:33], v[34:35] op_sel:[1,1] op_sel_hi:[0,1] neg_hi:[1,0]
	v_pk_fma_f32 v[32:33], v[32:33], v[34:35], v[36:37] op_sel_hi:[1,0,1]
	v_pk_mul_f32 v[36:37], v[180:181], v[34:35] op_sel:[1,1] op_sel_hi:[0,1] neg_lo:[0,1]
	v_pk_fma_f32 v[38:39], v[180:181], v[34:35], v[36:37] op_sel_hi:[1,0,1]
	v_xad_u32 v34, v50, 4, v10
	v_lshl_add_u32 v55, v34, 3, 0
	ds_read2_b64 v[34:37], v55 offset0:128 offset1:144
	v_pk_mul_f32 v[40:41], v[180:181], v[38:39] op_sel:[1,1] op_sel_hi:[0,1] neg_lo:[0,1]
	s_waitcnt lgkmcnt(0)
	v_pk_mul_f32 v[42:43], v[34:35], v[38:39] op_sel:[1,1] op_sel_hi:[0,1] neg_hi:[1,0]
	v_pk_fma_f32 v[34:35], v[34:35], v[38:39], v[42:43] op_sel_hi:[1,0,1]
	v_pk_fma_f32 v[42:43], v[180:181], v[38:39], v[40:41] op_sel_hi:[1,0,1]
	v_pk_mul_f32 v[38:39], v[36:37], v[42:43] op_sel:[1,1] op_sel_hi:[0,1] neg_hi:[1,0]
	v_pk_fma_f32 v[36:37], v[36:37], v[42:43], v[38:39] op_sel_hi:[1,0,1]
	v_xad_u32 v38, v50, 5, v10
	v_lshl_add_u32 v56, v38, 3, 0
	ds_read2_b64 v[38:41], v56 offset0:160 offset1:176
	v_pk_mul_f32 v[44:45], v[180:181], v[42:43] op_sel:[1,1] op_sel_hi:[0,1] neg_lo:[0,1]
	v_pk_fma_f32 v[42:43], v[180:181], v[42:43], v[44:45] op_sel_hi:[1,0,1]
	s_waitcnt lgkmcnt(0)
	v_pk_mul_f32 v[44:45], v[38:39], v[42:43] op_sel:[1,1] op_sel_hi:[0,1] neg_hi:[1,0]
	v_pk_fma_f32 v[38:39], v[38:39], v[42:43], v[44:45] op_sel_hi:[1,0,1]
	v_pk_mul_f32 v[44:45], v[180:181], v[42:43] op_sel:[1,1] op_sel_hi:[0,1] neg_lo:[0,1]
	v_pk_fma_f32 v[42:43], v[180:181], v[42:43], v[44:45] op_sel_hi:[1,0,1]
	v_pk_mul_f32 v[44:45], v[40:41], v[42:43] op_sel:[1,1] op_sel_hi:[0,1] neg_hi:[1,0]
	v_pk_fma_f32 v[40:41], v[40:41], v[42:43], v[44:45] op_sel_hi:[1,0,1]
	v_pk_mul_f32 v[44:45], v[180:181], v[42:43] op_sel:[1,1] op_sel_hi:[0,1] neg_lo:[0,1]
	v_pk_fma_f32 v[42:43], v[180:181], v[42:43], v[44:45] op_sel_hi:[1,0,1]
	v_xad_u32 v44, v50, 6, v10
	v_lshl_add_u32 v57, v44, 3, 0
	ds_read2_b64 v[44:47], v57 offset0:192 offset1:208
	v_pk_mul_f32 v[48:49], v[180:181], v[42:43] op_sel:[1,1] op_sel_hi:[0,1] neg_lo:[0,1]
	s_waitcnt lgkmcnt(0)
	v_pk_mul_f32 v[52:53], v[44:45], v[42:43] op_sel:[1,1] op_sel_hi:[0,1] neg_hi:[1,0]
	v_pk_fma_f32 v[44:45], v[44:45], v[42:43], v[52:53] op_sel_hi:[1,0,1]
	v_pk_fma_f32 v[52:53], v[180:181], v[42:43], v[48:49] op_sel_hi:[1,0,1]
	v_pk_mul_f32 v[42:43], v[46:47], v[52:53] op_sel:[1,1] op_sel_hi:[0,1] neg_hi:[1,0]
	v_pk_fma_f32 v[42:43], v[46:47], v[52:53], v[42:43] op_sel_hi:[1,0,1]
	v_xad_u32 v46, v50, 7, v10
	v_lshl_add_u32 v58, v46, 3, 0
	ds_read2_b64 v[46:49], v58 offset0:224 offset1:240
	v_pk_mul_f32 v[60:61], v[180:181], v[52:53] op_sel:[1,1] op_sel_hi:[0,1] neg_lo:[0,1]
	v_pk_fma_f32 v[52:53], v[180:181], v[52:53], v[60:61] op_sel_hi:[1,0,1]
	s_waitcnt lgkmcnt(0)
	v_pk_mul_f32 v[60:61], v[46:47], v[52:53] op_sel:[1,1] op_sel_hi:[0,1] neg_hi:[1,0]
	v_pk_fma_f32 v[46:47], v[46:47], v[52:53], v[60:61] op_sel_hi:[1,0,1]
	v_pk_mul_f32 v[60:61], v[180:181], v[52:53] op_sel:[1,1] op_sel_hi:[0,1] neg_lo:[0,1]
	v_pk_fma_f32 v[52:53], v[180:181], v[52:53], v[60:61] op_sel_hi:[1,0,1]
	v_pk_mul_f32 v[60:61], v[48:49], v[52:53] op_sel:[1,1] op_sel_hi:[0,1] neg_hi:[1,0]
	v_pk_fma_f32 v[48:49], v[48:49], v[52:53], v[60:61] op_sel_hi:[1,0,1]
	v_pk_mul_f32 v[60:61], v[180:181], v[52:53] op_sel:[1,1] op_sel_hi:[0,1] neg_lo:[0,1]
	v_pk_fma_f32 v[64:65], v[180:181], v[52:53], v[60:61] op_sel_hi:[1,0,1]
	v_xad_u32 v52, v50, 8, v10
	v_lshl_add_u32 v52, v52, 3, 0
	v_add_u32_e32 v59, 0x800, v52
	ds_read2_b64 v[60:63], v59 offset1:16
	v_pk_mul_f32 v[66:67], v[180:181], v[64:65] op_sel:[1,1] op_sel_hi:[0,1] neg_lo:[0,1]
	v_pk_fma_f32 v[66:67], v[180:181], v[64:65], v[66:67] op_sel_hi:[1,0,1]
	s_waitcnt lgkmcnt(0)
	v_pk_mul_f32 v[52:53], v[60:61], v[64:65] op_sel:[1,1] op_sel_hi:[0,1] neg_hi:[1,0]
	v_pk_fma_f32 v[52:53], v[60:61], v[64:65], v[52:53] op_sel_hi:[1,0,1]
	v_pk_mul_f32 v[60:61], v[62:63], v[66:67] op_sel:[1,1] op_sel_hi:[0,1] neg_hi:[1,0]
	v_pk_fma_f32 v[70:71], v[62:63], v[66:67], v[60:61] op_sel_hi:[1,0,1]
	v_xad_u32 v60, v50, 9, v10
	v_lshl_add_u32 v60, v60, 3, 0
	v_add_u32_e32 v60, 0x800, v60
	ds_read2_b64 v[62:65], v60 offset0:32 offset1:48
	v_pk_mul_f32 v[68:69], v[180:181], v[66:67] op_sel:[1,1] op_sel_hi:[0,1] neg_lo:[0,1]
	v_pk_fma_f32 v[66:67], v[180:181], v[66:67], v[68:69] op_sel_hi:[1,0,1]
	s_waitcnt lgkmcnt(0)
	v_pk_mul_f32 v[68:69], v[62:63], v[66:67] op_sel:[1,1] op_sel_hi:[0,1] neg_hi:[1,0]
	v_pk_fma_f32 v[72:73], v[62:63], v[66:67], v[68:69] op_sel_hi:[1,0,1]
	v_pk_mul_f32 v[62:63], v[180:181], v[66:67] op_sel:[1,1] op_sel_hi:[0,1] neg_lo:[0,1]
	v_pk_fma_f32 v[62:63], v[180:181], v[66:67], v[62:63] op_sel_hi:[1,0,1]
	v_pk_mul_f32 v[66:67], v[64:65], v[62:63] op_sel:[1,1] op_sel_hi:[0,1] neg_hi:[1,0]
	v_pk_fma_f32 v[74:75], v[64:65], v[62:63], v[66:67] op_sel_hi:[1,0,1]
	v_pk_mul_f32 v[64:65], v[180:181], v[62:63] op_sel:[1,1] op_sel_hi:[0,1] neg_lo:[0,1]
	v_pk_fma_f32 v[66:67], v[180:181], v[62:63], v[64:65] op_sel_hi:[1,0,1]
	v_xad_u32 v61, v50, 10, v10
	v_lshl_add_u32 v61, v61, 3, 0
	v_add_u32_e32 v61, 0x800, v61
	ds_read2_b64 v[62:65], v61 offset0:64 offset1:80
	v_pk_mul_f32 v[68:69], v[180:181], v[66:67] op_sel:[1,1] op_sel_hi:[0,1] neg_lo:[0,1]
	v_pk_fma_f32 v[68:69], v[180:181], v[66:67], v[68:69] op_sel_hi:[1,0,1]
	s_waitcnt lgkmcnt(0)
	v_pk_mul_f32 v[76:77], v[62:63], v[66:67] op_sel:[1,1] op_sel_hi:[0,1] neg_hi:[1,0]
	v_pk_fma_f32 v[76:77], v[62:63], v[66:67], v[76:77] op_sel_hi:[1,0,1]
	v_pk_mul_f32 v[62:63], v[64:65], v[68:69] op_sel:[1,1] op_sel_hi:[0,1] neg_hi:[1,0]
	v_pk_fma_f32 v[78:79], v[64:65], v[68:69], v[62:63] op_sel_hi:[1,0,1]
	v_xad_u32 v62, v50, 11, v10
	v_lshl_add_u32 v62, v62, 3, 0
	v_add_u32_e32 v62, 0x800, v62
	ds_read2_b64 v[64:67], v62 offset0:96 offset1:112
	v_pk_mul_f32 v[80:81], v[180:181], v[68:69] op_sel:[1,1] op_sel_hi:[0,1] neg_lo:[0,1]
	v_pk_fma_f32 v[68:69], v[180:181], v[68:69], v[80:81] op_sel_hi:[1,0,1]
	s_waitcnt lgkmcnt(0)
	v_pk_mul_f32 v[80:81], v[64:65], v[68:69] op_sel:[1,1] op_sel_hi:[0,1] neg_hi:[1,0]
	v_pk_fma_f32 v[80:81], v[64:65], v[68:69], v[80:81] op_sel_hi:[1,0,1]
	v_pk_mul_f32 v[64:65], v[180:181], v[68:69] op_sel:[1,1] op_sel_hi:[0,1] neg_lo:[0,1]
	v_pk_fma_f32 v[64:65], v[180:181], v[68:69], v[64:65] op_sel_hi:[1,0,1]
	v_pk_mul_f32 v[68:69], v[66:67], v[64:65] op_sel:[1,1] op_sel_hi:[0,1] neg_hi:[1,0]
	v_pk_fma_f32 v[82:83], v[66:67], v[64:65], v[68:69] op_sel_hi:[1,0,1]
	v_pk_mul_f32 v[66:67], v[180:181], v[64:65] op_sel:[1,1] op_sel_hi:[0,1] neg_lo:[0,1]
	v_pk_fma_f32 v[68:69], v[180:181], v[64:65], v[66:67] op_sel_hi:[1,0,1]
	v_xad_u32 v63, v50, 12, v10
	v_lshl_add_u32 v63, v63, 3, 0
	v_add_u32_e32 v63, 0x800, v63
	ds_read2_b64 v[64:67], v63 offset0:128 offset1:144
	v_pk_mul_f32 v[84:85], v[180:181], v[68:69] op_sel:[1,1] op_sel_hi:[0,1] neg_lo:[0,1]
	v_pk_fma_f32 v[84:85], v[180:181], v[68:69], v[84:85] op_sel_hi:[1,0,1]
	s_waitcnt lgkmcnt(0)
	v_pk_mul_f32 v[86:87], v[64:65], v[68:69] op_sel:[1,1] op_sel_hi:[0,1] neg_hi:[1,0]
	v_pk_fma_f32 v[86:87], v[64:65], v[68:69], v[86:87] op_sel_hi:[1,0,1]
	v_pk_mul_f32 v[64:65], v[66:67], v[84:85] op_sel:[1,1] op_sel_hi:[0,1] neg_hi:[1,0]
	v_pk_fma_f32 v[88:89], v[66:67], v[84:85], v[64:65] op_sel_hi:[1,0,1]
	v_xad_u32 v64, v50, 13, v10
	v_lshl_add_u32 v64, v64, 3, 0
	v_add_u32_e32 v64, 0x800, v64
	ds_read2_b64 v[66:69], v64 offset0:160 offset1:176
	v_pk_mul_f32 v[90:91], v[180:181], v[84:85] op_sel:[1,1] op_sel_hi:[0,1] neg_lo:[0,1]
	v_pk_fma_f32 v[84:85], v[180:181], v[84:85], v[90:91] op_sel_hi:[1,0,1]
	s_waitcnt lgkmcnt(0)
	v_pk_mul_f32 v[90:91], v[66:67], v[84:85] op_sel:[1,1] op_sel_hi:[0,1] neg_hi:[1,0]
	v_pk_fma_f32 v[90:91], v[66:67], v[84:85], v[90:91] op_sel_hi:[1,0,1]
	v_pk_mul_f32 v[66:67], v[180:181], v[84:85] op_sel:[1,1] op_sel_hi:[0,1] neg_lo:[0,1]
	v_pk_fma_f32 v[66:67], v[180:181], v[84:85], v[66:67] op_sel_hi:[1,0,1]
	v_pk_mul_f32 v[84:85], v[68:69], v[66:67] op_sel:[1,1] op_sel_hi:[0,1] neg_hi:[1,0]
	v_pk_fma_f32 v[84:85], v[68:69], v[66:67], v[84:85] op_sel_hi:[1,0,1]
	v_pk_mul_f32 v[68:69], v[180:181], v[66:67] op_sel:[1,1] op_sel_hi:[0,1] neg_lo:[0,1]
	v_pk_fma_f32 v[92:93], v[180:181], v[66:67], v[68:69] op_sel_hi:[1,0,1]
	v_xad_u32 v65, v50, 14, v10
	v_lshl_add_u32 v65, v65, 3, 0
	v_add_u32_e32 v65, 0x800, v65
	ds_read2_b64 v[66:69], v65 offset0:192 offset1:208
	v_pk_mul_f32 v[94:95], v[180:181], v[92:93] op_sel:[1,1] op_sel_hi:[0,1] neg_lo:[0,1]
	v_xad_u32 v10, v50, 15, v10
	s_waitcnt lgkmcnt(0)
	v_pk_mul_f32 v[96:97], v[66:67], v[92:93] op_sel:[1,1] op_sel_hi:[0,1] neg_hi:[1,0]
	v_lshl_add_u32 v10, v10, 3, 0
	v_pk_fma_f32 v[96:97], v[66:67], v[92:93], v[96:97] op_sel_hi:[1,0,1]
	v_pk_fma_f32 v[92:93], v[180:181], v[92:93], v[94:95] op_sel_hi:[1,0,1]
	v_pk_mul_f32 v[66:67], v[68:69], v[92:93] op_sel:[1,1] op_sel_hi:[0,1] neg_hi:[1,0]
	v_add_u32_e32 v101, 0x800, v10
	v_pk_fma_f32 v[94:95], v[68:69], v[92:93], v[66:67] op_sel_hi:[1,0,1]
	ds_read2_b64 v[66:69], v101 offset0:224 offset1:240
	v_pk_mul_f32 v[98:99], v[180:181], v[92:93] op_sel:[1,1] op_sel_hi:[0,1] neg_lo:[0,1]
	v_pk_fma_f32 v[92:93], v[180:181], v[92:93], v[98:99] op_sel_hi:[1,0,1]
	s_waitcnt lgkmcnt(0)
	v_pk_mul_f32 v[98:99], v[66:67], v[92:93] op_sel:[1,1] op_sel_hi:[0,1] neg_hi:[1,0]
	v_pk_fma_f32 v[66:67], v[66:67], v[92:93], v[98:99] op_sel_hi:[1,0,1]
	v_pk_mul_f32 v[98:99], v[180:181], v[92:93] op_sel:[1,1] op_sel_hi:[0,1] neg_lo:[0,1]
	v_pk_fma_f32 v[20:21], v[180:181], v[92:93], v[98:99] op_sel_hi:[1,0,1]
	v_pk_mul_f32 v[92:93], v[68:69], v[20:21] op_sel:[1,1] op_sel_hi:[0,1] neg_hi:[1,0]
	v_pk_fma_f32 v[68:69], v[68:69], v[20:21], v[92:93] op_sel_hi:[1,0,1]
	v_mov_b32_e32 v10, v1
	v_pk_add_f32 v[104:105], v[16:17], v[52:53]
	v_pk_add_f32 v[16:17], v[16:17], v[52:53] neg_lo:[0,1] neg_hi:[0,1]
	v_pk_add_f32 v[52:53], v[18:19], v[70:71]
	v_pk_add_f32 v[18:19], v[18:19], v[70:71] neg_lo:[0,1] neg_hi:[0,1]
	v_mov_b32_e32 v92, v164
	v_mov_b32_e32 v20, v165
	v_mov_b32_e32 v98, v166
	v_mov_b32_e32 v10, v167
	v_mov_b32_e32 v100, v168
	v_mov_b32_e32 v50, v169
	v_mov_b32_e32 v102, v170
	v_mov_b32_e32 v21, v171
	v_pk_mul_f32 v[70:71], v[102:103], v[18:19] op_sel:[0,1] op_sel_hi:[0,0] neg_lo:[0,1]
	v_pk_fma_f32 v[18:19], v[92:93], v[18:19], v[70:71] op_sel_hi:[0,1,1]
	v_pk_add_f32 v[70:71], v[22:23], v[72:73]
	v_pk_add_f32 v[22:23], v[22:23], v[72:73] neg_lo:[0,1] neg_hi:[0,1]
	v_pk_mul_f32 v[72:73], v[50:51], v[22:23] op_sel:[0,1] op_sel_hi:[0,0] neg_lo:[0,1]
	v_pk_fma_f32 v[22:23], v[20:21], v[22:23], v[72:73] op_sel_hi:[0,1,1]
	v_pk_add_f32 v[72:73], v[24:25], v[74:75]
	v_pk_add_f32 v[24:25], v[24:25], v[74:75] neg_lo:[0,1] neg_hi:[0,1]
	v_pk_mul_f32 v[74:75], v[100:101], v[24:25] op_sel:[0,1] op_sel_hi:[0,0] neg_lo:[0,1]
	v_pk_fma_f32 v[24:25], v[98:99], v[24:25], v[74:75] op_sel_hi:[0,1,1]
	v_pk_add_f32 v[74:75], v[28:29], v[76:77]
	v_pk_add_f32 v[28:29], v[28:29], v[76:77] neg_lo:[0,1] neg_hi:[0,1]
	v_pk_mul_f32 v[76:77], v[10:11], v[28:29] op_sel:[0,1] op_sel_hi:[0,0] neg_lo:[0,1]
	v_pk_fma_f32 v[28:29], v[10:11], v[28:29], v[76:77] op_sel_hi:[0,1,1]
	v_pk_add_f32 v[76:77], v[26:27], v[78:79]
	v_pk_add_f32 v[26:27], v[26:27], v[78:79] neg_lo:[0,1] neg_hi:[0,1]
	v_pk_mul_f32 v[78:79], v[98:99], v[26:27] op_sel:[0,1] op_sel_hi:[0,0] neg_lo:[0,1]
	v_pk_fma_f32 v[26:27], v[100:101], v[26:27], v[78:79] op_sel_hi:[0,1,1]
	v_pk_add_f32 v[78:79], v[30:31], v[80:81]
	v_pk_add_f32 v[30:31], v[30:31], v[80:81] neg_lo:[0,1] neg_hi:[0,1]
	v_pk_mul_f32 v[80:81], v[20:21], v[30:31] op_sel:[0,1] op_sel_hi:[0,0] neg_lo:[0,1]
	v_pk_fma_f32 v[30:31], v[50:51], v[30:31], v[80:81] op_sel_hi:[0,1,1]
	v_pk_add_f32 v[80:81], v[32:33], v[82:83]
	v_pk_add_f32 v[32:33], v[32:33], v[82:83] neg_lo:[0,1] neg_hi:[0,1]
	v_pk_mul_f32 v[82:83], v[92:93], v[32:33] op_sel:[0,1] op_sel_hi:[0,0] neg_lo:[0,1]
	v_pk_fma_f32 v[32:33], v[102:103], v[32:33], v[82:83] op_sel_hi:[0,1,1]
	v_pk_add_f32 v[82:83], v[34:35], v[86:87]
	v_pk_add_f32 v[34:35], v[34:35], v[86:87] neg_lo:[0,1] neg_hi:[0,1]
	v_xor_b32_e32 v86, 0x80000000, v35
	v_mov_b32_e32 v87, v34
	v_pk_add_f32 v[34:35], v[36:37], v[88:89]
	v_pk_add_f32 v[36:37], v[36:37], v[88:89] neg_lo:[0,1] neg_hi:[0,1]
	v_pk_mul_f32 v[88:89], v[92:93], v[36:37] op_sel:[0,1] op_sel_hi:[0,0] neg_lo:[0,1]
	v_pk_fma_f32 v[36:37], v[102:103], v[36:37], v[88:89] op_sel_hi:[0,1,1] neg_lo:[1,0,0] neg_hi:[1,0,0]
	v_pk_add_f32 v[88:89], v[38:39], v[90:91]
	v_pk_add_f32 v[38:39], v[38:39], v[90:91] neg_lo:[0,1] neg_hi:[0,1]
	v_pk_mul_f32 v[90:91], v[20:21], v[38:39] op_sel:[0,1] op_sel_hi:[0,0] neg_lo:[0,1]
	v_pk_fma_f32 v[38:39], v[50:51], v[38:39], v[90:91] op_sel_hi:[0,1,1] neg_lo:[1,0,0] neg_hi:[1,0,0]
	v_pk_add_f32 v[90:91], v[40:41], v[84:85]
	v_pk_add_f32 v[40:41], v[40:41], v[84:85] neg_lo:[0,1] neg_hi:[0,1]
	v_pk_mul_f32 v[84:85], v[98:99], v[40:41] op_sel:[0,1] op_sel_hi:[0,0] neg_lo:[0,1]
	v_pk_fma_f32 v[40:41], v[100:101], v[40:41], v[84:85] op_sel_hi:[0,1,1] neg_lo:[1,0,0] neg_hi:[1,0,0]
	v_pk_add_f32 v[84:85], v[44:45], v[96:97]
	v_pk_add_f32 v[44:45], v[44:45], v[96:97] neg_lo:[0,1] neg_hi:[0,1]
	v_pk_mul_f32 v[96:97], v[10:11], v[44:45] op_sel:[0,1] op_sel_hi:[0,0] neg_lo:[0,1]
	v_pk_fma_f32 v[44:45], v[10:11], v[44:45], v[96:97] op_sel_hi:[0,1,1] neg_lo:[1,0,0] neg_hi:[1,0,0]
	v_pk_add_f32 v[96:97], v[42:43], v[94:95]
	v_pk_add_f32 v[42:43], v[42:43], v[94:95] neg_lo:[0,1] neg_hi:[0,1]
	v_pk_mul_f32 v[94:95], v[100:101], v[42:43] op_sel:[0,1] op_sel_hi:[0,0] neg_lo:[0,1]
	v_pk_fma_f32 v[42:43], v[98:99], v[42:43], v[94:95] op_sel_hi:[0,1,1] neg_lo:[1,0,0] neg_hi:[1,0,0]
	v_pk_add_f32 v[94:95], v[46:47], v[66:67]
	v_pk_add_f32 v[46:47], v[46:47], v[66:67] neg_lo:[0,1] neg_hi:[0,1]
	v_pk_mul_f32 v[66:67], v[50:51], v[46:47] op_sel:[0,1] op_sel_hi:[0,0] neg_lo:[0,1]
	v_pk_fma_f32 v[46:47], v[20:21], v[46:47], v[66:67] op_sel_hi:[0,1,1] neg_lo:[1,0,0] neg_hi:[1,0,0]
	v_pk_add_f32 v[66:67], v[48:49], v[68:69]
	v_pk_add_f32 v[48:49], v[48:49], v[68:69] neg_lo:[0,1] neg_hi:[0,1]
	v_pk_mul_f32 v[68:69], v[102:103], v[48:49] op_sel:[0,1] op_sel_hi:[0,0] neg_lo:[0,1]
	v_pk_fma_f32 v[48:49], v[92:93], v[48:49], v[68:69] op_sel_hi:[0,1,1] neg_lo:[1,0,0] neg_hi:[1,0,0]
	v_pk_add_f32 v[92:93], v[52:53], v[34:35]
	v_pk_add_f32 v[34:35], v[52:53], v[34:35] neg_lo:[0,1] neg_hi:[0,1]
	v_pk_add_f32 v[68:69], v[104:105], v[82:83]
	v_pk_mul_f32 v[52:53], v[50:51], v[34:35] op_sel:[0,1] op_sel_hi:[0,0] neg_lo:[0,1]
	v_pk_fma_f32 v[34:35], v[20:21], v[34:35], v[52:53] op_sel_hi:[0,1,1]
	v_pk_add_f32 v[52:53], v[70:71], v[88:89]
	v_pk_add_f32 v[70:71], v[70:71], v[88:89] neg_lo:[0,1] neg_hi:[0,1]
	v_pk_add_f32 v[82:83], v[104:105], v[82:83] neg_lo:[0,1] neg_hi:[0,1]
	v_pk_mul_f32 v[88:89], v[10:11], v[70:71] op_sel:[0,1] op_sel_hi:[0,0] neg_lo:[0,1]
	v_pk_fma_f32 v[70:71], v[10:11], v[70:71], v[88:89] op_sel_hi:[0,1,1]
	v_pk_add_f32 v[88:89], v[72:73], v[90:91]
	v_pk_add_f32 v[72:73], v[72:73], v[90:91] neg_lo:[0,1] neg_hi:[0,1]
	v_pk_mul_f32 v[90:91], v[20:21], v[72:73] op_sel:[0,1] op_sel_hi:[0,0] neg_lo:[0,1]
	v_pk_fma_f32 v[72:73], v[50:51], v[72:73], v[90:91] op_sel_hi:[0,1,1]
	v_pk_add_f32 v[90:91], v[74:75], v[84:85]
	v_pk_add_f32 v[74:75], v[74:75], v[84:85] neg_lo:[0,1] neg_hi:[0,1]
	v_xor_b32_e32 v84, 0x80000000, v75
	v_mov_b32_e32 v85, v74
	v_pk_add_f32 v[74:75], v[76:77], v[96:97]
	v_pk_add_f32 v[76:77], v[76:77], v[96:97] neg_lo:[0,1] neg_hi:[0,1]
	v_pk_mul_f32 v[96:97], v[20:21], v[76:77] op_sel:[0,1] op_sel_hi:[0,0] neg_lo:[0,1]
	v_pk_fma_f32 v[76:77], v[50:51], v[76:77], v[96:97] op_sel_hi:[0,1,1] neg_lo:[1,0,0] neg_hi:[1,0,0]
	v_pk_add_f32 v[96:97], v[78:79], v[94:95]
	v_pk_add_f32 v[78:79], v[78:79], v[94:95] neg_lo:[0,1] neg_hi:[0,1]
	v_pk_mul_f32 v[94:95], v[10:11], v[78:79] op_sel:[0,1] op_sel_hi:[0,0] neg_lo:[0,1]
	v_pk_fma_f32 v[78:79], v[10:11], v[78:79], v[94:95] op_sel_hi:[0,1,1] neg_lo:[1,0,0] neg_hi:[1,0,0]
	v_pk_add_f32 v[94:95], v[80:81], v[66:67]
	v_pk_add_f32 v[66:67], v[80:81], v[66:67] neg_lo:[0,1] neg_hi:[0,1]
	v_pk_mul_f32 v[80:81], v[50:51], v[66:67] op_sel:[0,1] op_sel_hi:[0,0] neg_lo:[0,1]
	v_pk_fma_f32 v[66:67], v[20:21], v[66:67], v[80:81] op_sel_hi:[0,1,1] neg_lo:[1,0,0] neg_hi:[1,0,0]
	v_pk_add_f32 v[80:81], v[68:69], v[90:91]
	v_pk_add_f32 v[68:69], v[68:69], v[90:91] neg_lo:[0,1] neg_hi:[0,1]
	v_pk_add_f32 v[90:91], v[92:93], v[74:75]
	v_pk_add_f32 v[74:75], v[92:93], v[74:75] neg_lo:[0,1] neg_hi:[0,1]
	v_pk_mul_f32 v[92:93], v[10:11], v[74:75] op_sel:[0,1] op_sel_hi:[0,0] neg_lo:[0,1]
	v_pk_fma_f32 v[74:75], v[10:11], v[74:75], v[92:93] op_sel_hi:[0,1,1]
	v_pk_add_f32 v[92:93], v[52:53], v[96:97]
	v_pk_add_f32 v[52:53], v[52:53], v[96:97] neg_lo:[0,1] neg_hi:[0,1]
	v_xor_b32_e32 v96, 0x80000000, v53
	v_mov_b32_e32 v97, v52
	v_pk_add_f32 v[52:53], v[88:89], v[94:95]
	v_pk_add_f32 v[88:89], v[88:89], v[94:95] neg_lo:[0,1] neg_hi:[0,1]
	v_pk_mul_f32 v[94:95], v[10:11], v[88:89] op_sel:[0,1] op_sel_hi:[0,0] neg_lo:[0,1]
	v_pk_fma_f32 v[88:89], v[10:11], v[88:89], v[94:95] op_sel_hi:[0,1,1] neg_lo:[1,0,0] neg_hi:[1,0,0]
	v_pk_add_f32 v[94:95], v[80:81], v[92:93]
	v_pk_add_f32 v[80:81], v[80:81], v[92:93] neg_lo:[0,1] neg_hi:[0,1]
	v_pk_add_f32 v[92:93], v[90:91], v[52:53]
	v_pk_add_f32 v[52:53], v[90:91], v[52:53] neg_lo:[0,1] neg_hi:[0,1]
	v_xor_b32_e32 v90, 0x80000000, v53
	v_mov_b32_e32 v91, v52
	v_pk_add_f32 v[52:53], v[94:95], v[92:93]
	v_pk_add_f32 v[92:93], v[94:95], v[92:93] neg_lo:[0,1] neg_hi:[0,1]
	v_pk_add_f32 v[94:95], v[80:81], v[90:91]
	v_pk_add_f32 v[80:81], v[80:81], v[90:91] neg_lo:[0,1] neg_hi:[0,1]
	v_pk_add_f32 v[90:91], v[68:69], v[96:97]
	v_pk_add_f32 v[68:69], v[68:69], v[96:97] neg_lo:[0,1] neg_hi:[0,1]
	v_pk_add_f32 v[96:97], v[74:75], v[88:89]
	v_pk_add_f32 v[74:75], v[74:75], v[88:89] neg_lo:[0,1] neg_hi:[0,1]
	v_xor_b32_e32 v88, 0x80000000, v75
	v_mov_b32_e32 v89, v74
	v_pk_add_f32 v[74:75], v[90:91], v[96:97]
	v_pk_add_f32 v[90:91], v[90:91], v[96:97] neg_lo:[0,1] neg_hi:[0,1]
	v_pk_add_f32 v[96:97], v[68:69], v[88:89]
	v_pk_add_f32 v[68:69], v[68:69], v[88:89] neg_lo:[0,1] neg_hi:[0,1]
	v_pk_add_f32 v[88:89], v[82:83], v[84:85]
	v_pk_add_f32 v[82:83], v[82:83], v[84:85] neg_lo:[0,1] neg_hi:[0,1]
	v_pk_add_f32 v[84:85], v[34:35], v[76:77]
	v_pk_add_f32 v[34:35], v[34:35], v[76:77] neg_lo:[0,1] neg_hi:[0,1]
	v_pk_mul_f32 v[76:77], v[10:11], v[34:35] op_sel:[0,1] op_sel_hi:[0,0] neg_lo:[0,1]
	v_pk_fma_f32 v[34:35], v[10:11], v[34:35], v[76:77] op_sel_hi:[0,1,1]
	v_pk_add_f32 v[76:77], v[70:71], v[78:79]
	v_pk_add_f32 v[70:71], v[70:71], v[78:79] neg_lo:[0,1] neg_hi:[0,1]
	v_xor_b32_e32 v78, 0x80000000, v71
	v_mov_b32_e32 v79, v70
	v_pk_add_f32 v[70:71], v[72:73], v[66:67]
	v_pk_add_f32 v[66:67], v[72:73], v[66:67] neg_lo:[0,1] neg_hi:[0,1]
	v_pk_mul_f32 v[72:73], v[10:11], v[66:67] op_sel:[0,1] op_sel_hi:[0,0] neg_lo:[0,1]
	v_pk_fma_f32 v[66:67], v[10:11], v[66:67], v[72:73] op_sel_hi:[0,1,1] neg_lo:[1,0,0] neg_hi:[1,0,0]
	v_pk_add_f32 v[72:73], v[88:89], v[76:77]
	v_pk_add_f32 v[76:77], v[88:89], v[76:77] neg_lo:[0,1] neg_hi:[0,1]
	v_pk_add_f32 v[88:89], v[84:85], v[70:71]
	v_pk_add_f32 v[70:71], v[84:85], v[70:71] neg_lo:[0,1] neg_hi:[0,1]
	v_xor_b32_e32 v84, 0x80000000, v71
	v_mov_b32_e32 v85, v70
	v_pk_add_f32 v[70:71], v[72:73], v[88:89]
	v_pk_add_f32 v[72:73], v[72:73], v[88:89] neg_lo:[0,1] neg_hi:[0,1]
	v_pk_add_f32 v[88:89], v[76:77], v[84:85]
	v_pk_add_f32 v[76:77], v[76:77], v[84:85] neg_lo:[0,1] neg_hi:[0,1]
	v_pk_add_f32 v[84:85], v[82:83], v[78:79]
	v_pk_add_f32 v[78:79], v[82:83], v[78:79] neg_lo:[0,1] neg_hi:[0,1]
	v_pk_add_f32 v[82:83], v[34:35], v[66:67]
	v_pk_add_f32 v[34:35], v[34:35], v[66:67] neg_lo:[0,1] neg_hi:[0,1]
	v_xor_b32_e32 v66, 0x80000000, v35
	v_mov_b32_e32 v67, v34
	v_pk_add_f32 v[34:35], v[84:85], v[82:83]
	v_pk_add_f32 v[82:83], v[84:85], v[82:83] neg_lo:[0,1] neg_hi:[0,1]
	v_pk_add_f32 v[84:85], v[78:79], v[66:67]
	v_pk_add_f32 v[66:67], v[78:79], v[66:67] neg_lo:[0,1] neg_hi:[0,1]
	v_pk_add_f32 v[78:79], v[16:17], v[86:87]
	v_pk_add_f32 v[16:17], v[16:17], v[86:87] neg_lo:[0,1] neg_hi:[0,1]
	v_pk_add_f32 v[86:87], v[18:19], v[36:37]
	v_pk_add_f32 v[18:19], v[18:19], v[36:37] neg_lo:[0,1] neg_hi:[0,1]
	v_pk_mul_f32 v[36:37], v[50:51], v[18:19] op_sel:[0,1] op_sel_hi:[0,0] neg_lo:[0,1]
	v_pk_fma_f32 v[18:19], v[20:21], v[18:19], v[36:37] op_sel_hi:[0,1,1]
	v_pk_add_f32 v[36:37], v[22:23], v[38:39]
	v_pk_add_f32 v[22:23], v[22:23], v[38:39] neg_lo:[0,1] neg_hi:[0,1]
	v_pk_mul_f32 v[38:39], v[10:11], v[22:23] op_sel:[0,1] op_sel_hi:[0,0] neg_lo:[0,1]
	v_pk_fma_f32 v[22:23], v[10:11], v[22:23], v[38:39] op_sel_hi:[0,1,1]
	v_pk_add_f32 v[38:39], v[24:25], v[40:41]
	v_pk_add_f32 v[24:25], v[24:25], v[40:41] neg_lo:[0,1] neg_hi:[0,1]
	v_pk_mul_f32 v[40:41], v[20:21], v[24:25] op_sel:[0,1] op_sel_hi:[0,0] neg_lo:[0,1]
	v_pk_fma_f32 v[24:25], v[50:51], v[24:25], v[40:41] op_sel_hi:[0,1,1]
	v_pk_add_f32 v[40:41], v[28:29], v[44:45]
	v_pk_add_f32 v[28:29], v[28:29], v[44:45] neg_lo:[0,1] neg_hi:[0,1]
	v_xor_b32_e32 v44, 0x80000000, v29
	v_mov_b32_e32 v45, v28
	v_pk_add_f32 v[28:29], v[26:27], v[42:43]
	v_pk_add_f32 v[26:27], v[26:27], v[42:43] neg_lo:[0,1] neg_hi:[0,1]
	v_pk_mul_f32 v[42:43], v[20:21], v[26:27] op_sel:[0,1] op_sel_hi:[0,0] neg_lo:[0,1]
	v_pk_fma_f32 v[26:27], v[50:51], v[26:27], v[42:43] op_sel_hi:[0,1,1] neg_lo:[1,0,0] neg_hi:[1,0,0]
	v_pk_add_f32 v[42:43], v[30:31], v[46:47]
	v_pk_add_f32 v[30:31], v[30:31], v[46:47] neg_lo:[0,1] neg_hi:[0,1]
	v_pk_mul_f32 v[46:47], v[10:11], v[30:31] op_sel:[0,1] op_sel_hi:[0,0] neg_lo:[0,1]
	v_pk_fma_f32 v[30:31], v[10:11], v[30:31], v[46:47] op_sel_hi:[0,1,1] neg_lo:[1,0,0] neg_hi:[1,0,0]
	v_pk_add_f32 v[46:47], v[32:33], v[48:49]
	v_pk_add_f32 v[32:33], v[32:33], v[48:49] neg_lo:[0,1] neg_hi:[0,1]
	v_pk_mul_f32 v[48:49], v[50:51], v[32:33] op_sel:[0,1] op_sel_hi:[0,0] neg_lo:[0,1]
	v_pk_fma_f32 v[20:21], v[20:21], v[32:33], v[48:49] op_sel_hi:[0,1,1] neg_lo:[1,0,0] neg_hi:[1,0,0]
	v_pk_add_f32 v[48:49], v[86:87], v[28:29]
	v_pk_add_f32 v[28:29], v[86:87], v[28:29] neg_lo:[0,1] neg_hi:[0,1]
	v_pk_add_f32 v[32:33], v[78:79], v[40:41]
	v_pk_add_f32 v[40:41], v[78:79], v[40:41] neg_lo:[0,1] neg_hi:[0,1]
	v_pk_mul_f32 v[78:79], v[10:11], v[28:29] op_sel:[0,1] op_sel_hi:[0,0] neg_lo:[0,1]
	v_pk_fma_f32 v[28:29], v[10:11], v[28:29], v[78:79] op_sel_hi:[0,1,1]
	v_pk_add_f32 v[78:79], v[36:37], v[42:43]
	v_pk_add_f32 v[36:37], v[36:37], v[42:43] neg_lo:[0,1] neg_hi:[0,1]
	v_xor_b32_e32 v42, 0x80000000, v37
	v_mov_b32_e32 v43, v36
	v_pk_add_f32 v[36:37], v[38:39], v[46:47]
	v_pk_add_f32 v[38:39], v[38:39], v[46:47] neg_lo:[0,1] neg_hi:[0,1]
	v_pk_mul_f32 v[46:47], v[10:11], v[38:39] op_sel:[0,1] op_sel_hi:[0,0] neg_lo:[0,1]
	v_pk_fma_f32 v[38:39], v[10:11], v[38:39], v[46:47] op_sel_hi:[0,1,1] neg_lo:[1,0,0] neg_hi:[1,0,0]
	v_pk_add_f32 v[46:47], v[32:33], v[78:79]
	v_pk_add_f32 v[32:33], v[32:33], v[78:79] neg_lo:[0,1] neg_hi:[0,1]
	v_pk_add_f32 v[78:79], v[48:49], v[36:37]
	v_pk_add_f32 v[36:37], v[48:49], v[36:37] neg_lo:[0,1] neg_hi:[0,1]
	v_pk_add_f32 v[86:87], v[32:33], v[36:37] op_sel:[0,1] op_sel_hi:[1,0] neg_lo:[0,1]
	v_pk_add_f32 v[32:33], v[32:33], v[36:37] op_sel:[0,1] op_sel_hi:[1,0] neg_hi:[0,1]
	v_pk_add_f32 v[48:49], v[40:41], v[42:43]
	v_pk_add_f32 v[40:41], v[40:41], v[42:43] neg_lo:[0,1] neg_hi:[0,1]
	v_pk_add_f32 v[42:43], v[28:29], v[38:39]
	v_pk_add_f32 v[28:29], v[28:29], v[38:39] neg_lo:[0,1] neg_hi:[0,1]
	v_pk_add_f32 v[36:37], v[46:47], v[78:79] neg_lo:[0,1] neg_hi:[0,1]
	v_xor_b32_e32 v38, 0x80000000, v29
	v_mov_b32_e32 v39, v28
	v_pk_add_f32 v[28:29], v[48:49], v[42:43]
	v_pk_add_f32 v[42:43], v[48:49], v[42:43] neg_lo:[0,1] neg_hi:[0,1]
	v_pk_add_f32 v[48:49], v[40:41], v[38:39]
	v_pk_add_f32 v[38:39], v[40:41], v[38:39] neg_lo:[0,1] neg_hi:[0,1]
	v_pk_add_f32 v[40:41], v[16:17], v[44:45]
	v_pk_add_f32 v[16:17], v[16:17], v[44:45] neg_lo:[0,1] neg_hi:[0,1]
	v_pk_add_f32 v[44:45], v[18:19], v[26:27]
	v_pk_add_f32 v[18:19], v[18:19], v[26:27] neg_lo:[0,1] neg_hi:[0,1]
	v_pk_mul_f32 v[26:27], v[10:11], v[18:19] op_sel:[0,1] op_sel_hi:[0,0] neg_lo:[0,1]
	v_pk_fma_f32 v[18:19], v[10:11], v[18:19], v[26:27] op_sel_hi:[0,1,1]
	v_pk_add_f32 v[26:27], v[22:23], v[30:31]
	v_pk_add_f32 v[22:23], v[22:23], v[30:31] neg_lo:[0,1] neg_hi:[0,1]
	v_xor_b32_e32 v30, 0x80000000, v23
	v_mov_b32_e32 v31, v22
	v_pk_add_f32 v[22:23], v[24:25], v[20:21]
	v_pk_add_f32 v[20:21], v[24:25], v[20:21] neg_lo:[0,1] neg_hi:[0,1]
	v_pk_mul_f32 v[24:25], v[10:11], v[20:21] op_sel:[0,1] op_sel_hi:[0,0] neg_lo:[0,1]
	v_pk_fma_f32 v[20:21], v[10:11], v[20:21], v[24:25] op_sel_hi:[0,1,1] neg_lo:[1,0,0] neg_hi:[1,0,0]
	v_pk_add_f32 v[24:25], v[40:41], v[26:27]
	v_pk_add_f32 v[26:27], v[40:41], v[26:27] neg_lo:[0,1] neg_hi:[0,1]
	v_pk_add_f32 v[40:41], v[44:45], v[22:23]
	v_pk_add_f32 v[22:23], v[44:45], v[22:23] neg_lo:[0,1] neg_hi:[0,1]
	v_xor_b32_e32 v44, 0x80000000, v23
	v_mov_b32_e32 v45, v22
	v_pk_add_f32 v[22:23], v[24:25], v[40:41]
	v_pk_add_f32 v[24:25], v[24:25], v[40:41] neg_lo:[0,1] neg_hi:[0,1]
	v_pk_add_f32 v[40:41], v[26:27], v[44:45]
	v_pk_add_f32 v[26:27], v[26:27], v[44:45] neg_lo:[0,1] neg_hi:[0,1]
	v_pk_add_f32 v[44:45], v[16:17], v[30:31]
	v_pk_add_f32 v[16:17], v[16:17], v[30:31] neg_lo:[0,1] neg_hi:[0,1]
	v_pk_add_f32 v[30:31], v[18:19], v[20:21]
	v_pk_add_f32 v[18:19], v[18:19], v[20:21] neg_lo:[0,1] neg_hi:[0,1]
	v_xor_b32_e32 v20, 0x80000000, v19
	v_mov_b32_e32 v21, v18
	v_pk_add_f32 v[18:19], v[44:45], v[30:31]
	v_pk_add_f32 v[30:31], v[44:45], v[30:31] neg_lo:[0,1] neg_hi:[0,1]
	v_pk_add_f32 v[44:45], v[16:17], v[20:21]
	v_pk_add_f32 v[16:17], v[16:17], v[20:21] neg_lo:[0,1] neg_hi:[0,1]
	v_pk_add_f32 v[20:21], v[46:47], v[78:79]
	ds_write2_b64 v13, v[52:53], v[20:21] offset1:16
	ds_write2_b64 v15, v[70:71], v[22:23] offset0:32 offset1:48
	ds_write2_b64 v51, v[74:75], v[28:29] offset0:64 offset1:80
	ds_write2_b64 v54, v[34:35], v[18:19] offset0:96 offset1:112
	ds_write2_b64 v55, v[94:95], v[86:87] offset0:128 offset1:144
	ds_write2_b64 v56, v[88:89], v[40:41] offset0:160 offset1:176
	ds_write2_b64 v57, v[96:97], v[48:49] offset0:192 offset1:208
	ds_write2_b64 v58, v[84:85], v[44:45] offset0:224 offset1:240
	ds_write2_b64 v59, v[92:93], v[36:37] offset1:16
	ds_write2_b64 v60, v[72:73], v[24:25] offset0:32 offset1:48
	ds_write2_b64 v61, v[90:91], v[42:43] offset0:64 offset1:80
	ds_write2_b64 v62, v[82:83], v[30:31] offset0:96 offset1:112
	ds_write2_b64 v63, v[80:81], v[32:33] offset0:128 offset1:144
	ds_write2_b64 v64, v[76:77], v[26:27] offset0:160 offset1:176
	ds_write2_b64 v65, v[68:69], v[38:39] offset0:192 offset1:208
	ds_write2_b64 v101, v[66:67], v[16:17] offset0:224 offset1:240
	v_mov_b32_e32 v10, v173
	s_waitcnt lgkmcnt(0)
	s_barrier
	v_mov_b32_e32 v58, v178
	v_mov_b32_e32 v59, v179
	v_lshl_add_u32 v10, v10, 3, 0
	ds_read_b64 v[34:35], v10
	ds_read_b64 v[36:37], v10 offset:4224
	ds_read_b64 v[38:39], v10 offset:8448
	ds_read_b64 v[40:41], v10 offset:12672
	ds_read_b64 v[42:43], v10 offset:16896
	ds_read_b64 v[44:45], v10 offset:21120
	ds_read_b64 v[50:51], v10 offset:25344
	ds_read_b64 v[52:53], v10 offset:29568
	ds_read_b64 v[54:55], v10 offset:33792
	ds_read_b64 v[56:57], v10 offset:38016
	ds_read_b64 v[64:65], v10 offset:42240
	ds_read_b64 v[74:75], v10 offset:46464
	ds_read_b64 v[76:77], v10 offset:50688
	ds_read_b64 v[78:79], v10 offset:54912
	ds_read_b64 v[80:81], v10 offset:59136
	ds_read_b64 v[82:83], v10 offset:63360
	v_add_u32_e32 v13, 0x10800, v10
	v_add_u32_e32 v15, 0x11880, v10
	v_add_u32_e32 v16, 0x12900, v10
	v_add_u32_e32 v17, 0x13980, v10
	ds_read_b64 v[84:85], v13
	ds_read_b64 v[86:87], v15
	ds_read_b64 v[88:89], v16
	ds_read_b64 v[92:93], v17
	v_add_u32_e32 v13, 0x14a00, v10
	v_add_u32_e32 v15, 0x15a80, v10
	v_add_u32_e32 v16, 0x16b00, v10
	v_add_u32_e32 v17, 0x17b80, v10
	ds_read_b64 v[96:97], v13
	ds_read_b64 v[98:99], v15
	ds_read_b64 v[94:95], v16
	ds_read_b64 v[90:91], v17
	v_add_u32_e32 v13, 0x18c00, v10
	v_add_u32_e32 v15, 0x19c80, v10
	v_add_u32_e32 v16, 0x1ad00, v10
	v_add_u32_e32 v17, 0x1bd80, v10
	ds_read_b64 v[72:73], v13
	ds_read_b64 v[70:71], v15
	ds_read_b64 v[68:69], v16
	ds_read_b64 v[66:67], v17
	v_add_u32_e32 v13, 0x1ce00, v10
	v_add_u32_e32 v15, 0x1de80, v10
	v_add_u32_e32 v16, 0x1ef00, v10
	v_add_u32_e32 v10, 0x1ff80, v10
	ds_read_b64 v[62:63], v13
	ds_read_b64 v[60:61], v15
	ds_read_b64 v[100:101], v16
	ds_read_b64 v[102:103], v10
	s_mov_b32 s43, s95
	v_mov_b32_e32 v10, v1
	s_lshl_b64 s[0:1], s[42:43], 2
	v_readlane_b32 s2, v251, 46
	s_add_u32 s0, s2, s0
	v_readlane_b32 s2, v251, 48
	v_readlane_b32 s6, v251, 52
	v_mov_b32_e32 v24, v164
	v_mov_b32_e32 v32, v165
	v_mov_b32_e32 v28, v166
	v_mov_b32_e32 v46, v167
	v_mov_b32_e32 v48, v168
	v_mov_b32_e32 v30, v169
	v_mov_b32_e32 v26, v170
	v_mov_b32_e32 v10, v171
	v_mov_b32_e32 v16, v183
	v_mov_b32_e32 v19, v184
	s_addc_u32 s1, s2, s1
	v_readlane_b32 s7, v251, 53
	s_waitcnt lgkmcnt(0)
	s_barrier
	global_load_dword v13, v11, s[0:1]
	s_and_b64 s[0:1], s[6:7], exec
	s_movk_i32 s0, 0x800
	s_cselect_b32 s2, 0x400, s0
	v_readlane_b32 s24, v251, 50
	s_add_i32 s4, s2, s24
	s_mul_i32 s0, s4, 0x8200
	v_readlane_b32 s3, v251, 18
	s_mul_hi_i32 s1, s4, 0x8200
	s_add_u32 s0, s3, s0
	v_readlane_b32 s3, v251, 20
	s_addc_u32 s1, s3, s1
	s_lshl_b32 s2, s2, 2
	v_mov_b32_e32 v10, s2
	v_readlane_b32 s2, v251, 42
	v_readlane_b32 s3, v251, 43
	v_readlane_b32 s8, v250, 23
	v_readlane_b32 s9, v250, 24
	v_ashrrev_i32_e32 v15, 31, v14
	v_lshl_add_u64 v[22:23], v[14:15], 2, s[70:71]
	v_readlane_b32 s22, v250, 37
	global_load_dword v197, v10, s[2:3]
	s_add_i32 s2, s4, 0xc00
	s_ashr_i32 s3, s2, 31
	s_lshl_b64 s[2:3], s[2:3], 2
	s_add_u32 s2, s8, s2
	s_addc_u32 s3, s9, s3
	global_load_dword v198, v11, s[2:3]
	s_add_i32 s2, s4, 0x1800
	s_ashr_i32 s3, s2, 31
	s_lshl_b64 s[2:3], s[2:3], 2
	s_add_u32 s2, s8, s2
	s_addc_u32 s3, s9, s3
	global_load_dword v199, v11, s[2:3]
	v_readlane_b32 s2, v251, 40
	v_readlane_b32 s3, v251, 41
	v_cmp_lt_i32_e32 vcc, 0, v14
	v_mov_b32_e32 v17, 0
	v_lshl_add_u64 v[20:21], v[14:15], 1, s[0:1]
	v_mov_b32_e32 v18, 0
	v_readlane_b32 s25, v251, 51
	global_load_dword v200, v10, s[2:3]
	v_readlane_b32 s10, v250, 25
	v_lshlrev_b32_e32 v241, 1, v14
	v_lshlrev_b32_e32 v242, 2, v14
	v_add_u32_e32 v242, 0x1000, v242
	global_load_dword v190, v242, s[70:71] offset:-4096
	global_load_ushort v202, v241, s[0:1] offset:-2
	global_load_ushort v203, v241, s[0:1]
	global_load_ushort v204, v241, s[0:1] offset:2
	global_load_dword v205, v242, s[64:65] offset:-4096
	global_load_dword v206, v242, s[70:71] offset:-2048
	global_load_ushort v207, v241, s[0:1] offset:1022
	global_load_ushort v208, v241, s[0:1] offset:1024
	global_load_ushort v209, v241, s[0:1] offset:1026
	global_load_dword v210, v242, s[64:65] offset:-2048
	global_load_dword v211, v242, s[70:71]
	global_load_ushort v212, v241, s[0:1] offset:2046
	global_load_ushort v213, v241, s[0:1] offset:2048
	global_load_ushort v214, v241, s[0:1] offset:2050
	global_load_dword v215, v242, s[64:65]
	global_load_dword v216, v242, s[70:71] offset:2048
	global_load_ushort v217, v241, s[0:1] offset:3070
	global_load_ushort v218, v241, s[0:1] offset:3072
	global_load_ushort v219, v241, s[0:1] offset:3074
	global_load_dword v220, v242, s[64:65] offset:2048
	v_lshlrev_b32_e32 v241, 1, v14
	v_add_u32_e32 v241, 0x1000, v241
	v_lshlrev_b32_e32 v242, 2, v14
	v_add_u32_e32 v242, 0x3000, v242
	global_load_dword v221, v242, s[70:71] offset:-4096
	global_load_ushort v222, v241, s[0:1] offset:-2
	global_load_ushort v223, v241, s[0:1]
	global_load_ushort v224, v241, s[0:1] offset:2
	global_load_dword v225, v242, s[64:65] offset:-4096
	global_load_dword v226, v242, s[70:71] offset:-2048
	global_load_ushort v227, v241, s[0:1] offset:1022
	global_load_ushort v228, v241, s[0:1] offset:1024
	global_load_ushort v229, v241, s[0:1] offset:1026
	global_load_dword v230, v242, s[64:65] offset:-2048
	global_load_dword v231, v242, s[70:71]
	global_load_ushort v232, v241, s[0:1] offset:2046
	global_load_ushort v233, v241, s[0:1] offset:2048
	global_load_ushort v234, v241, s[0:1] offset:2050
	global_load_dword v235, v242, s[64:65]
	global_load_dword v236, v242, s[70:71] offset:2048
	global_load_ushort v237, v241, s[0:1] offset:3070
	global_load_ushort v238, v241, s[0:1] offset:3072
	global_load_ushort v239, v241, s[0:1] offset:3074
	global_load_dword v240, v242, s[64:65] offset:2048
	s_waitcnt vmcnt(20)
	v_mov_b32_e32 v10, v190
	v_readlane_b32 s11, v250, 26
	v_readlane_b32 s12, v250, 27
	v_readlane_b32 s13, v250, 28
	v_readlane_b32 s14, v250, 29
	v_readlane_b32 s15, v250, 30
	v_readlane_b32 s16, v250, 31
	v_readlane_b32 s17, v250, 32
	v_readlane_b32 s18, v250, 33
	v_readlane_b32 s19, v250, 34
	v_readlane_b32 s20, v250, 35
	v_readlane_b32 s21, v250, 36
	v_readlane_b32 s23, v250, 38
	s_and_saveexec_b64 s[2:3], vcc
	s_movk_i32 s22, 0x3fff
	s_cbranch_execz .LBB0_636
	v_mov_b32_e32 v18, v202
	s_nop 0
	v_lshlrev_b32_e32 v18, 16, v18

.LBB0_638:
	s_or_b64 exec, exec, s[2:3]
	v_add_f32_e32 v6, 0, v6
	v_add_f32_e32 v6, v6, v7
	v_add_f32_e32 v6, v6, v8
	v_add_f32_e32 v6, v6, v9
	v_add_f32_e32 v2, v6, v2
	v_add_f32_e32 v2, v2, v3
	v_add_f32_e32 v2, v2, v4
	v_add_f32_e32 v27, v2, v5
	v_pk_fma_f32 v[2:3], v[58:59], s[90:91], v[58:59] op_sel:[1,0,0] op_sel_hi:[0,1,1]
	v_pk_mul_f32 v[4:5], v[58:59], v[2:3] op_sel:[1,1] op_sel_hi:[0,1] neg_lo:[0,1]
	v_pk_fma_f32 v[4:5], v[58:59], v[2:3], v[4:5] op_sel_hi:[1,0,1]
	s_xor_b64 s[2:3], s[6:7], -1
	v_pk_mul_f32 v[6:7], v[58:59], v[4:5] op_sel:[1,1] op_sel_hi:[0,1] neg_lo:[0,1]
	v_pk_fma_f32 v[6:7], v[58:59], v[4:5], v[6:7] op_sel_hi:[1,0,1]
	s_brev_b32 s6, 28
	v_pk_mul_f32 v[8:9], v[58:59], v[6:7] op_sel:[1,1] op_sel_hi:[0,1] neg_lo:[0,1]
	v_pk_fma_f32 v[104:105], v[58:59], v[6:7], v[8:9] op_sel_hi:[1,0,1]
	v_div_scale_f32 v29, s[4:5], v27, v27, s6
	v_pk_mul_f32 v[8:9], v[58:59], v[104:105] op_sel:[1,1] op_sel_hi:[0,1] neg_lo:[0,1]
	v_pk_fma_f32 v[106:107], v[58:59], v[104:105], v[8:9] op_sel_hi:[1,0,1]
	s_mov_b32 s4, s45
	v_pk_mul_f32 v[8:9], v[58:59], v[106:107] op_sel:[1,1] op_sel_hi:[0,1] neg_lo:[0,1]
	v_pk_fma_f32 v[108:109], v[58:59], v[106:107], v[8:9] op_sel_hi:[1,0,1]
	s_mov_b32 s5, s94
	v_pk_mul_f32 v[8:9], v[58:59], v[108:109] op_sel:[1,1] op_sel_hi:[0,1] neg_lo:[0,1]
	v_pk_fma_f32 v[110:111], v[58:59], v[108:109], v[8:9] op_sel_hi:[1,0,1]
	s_mov_b32 s44, s94
	v_pk_mul_f32 v[8:9], v[58:59], v[110:111] op_sel:[1,1] op_sel_hi:[0,1] neg_lo:[0,1]
	v_pk_fma_f32 v[112:113], v[58:59], v[110:111], v[8:9] op_sel_hi:[1,0,1]
	v_rcp_f32_e32 v31, v29
	v_pk_mul_f32 v[8:9], v[58:59], v[112:113] op_sel:[1,1] op_sel_hi:[0,1] neg_lo:[0,1]
	v_pk_fma_f32 v[114:115], v[58:59], v[112:113], v[8:9] op_sel_hi:[1,0,1]
	v_fma_f32 v33, -v29, v31, 1.0
	v_pk_mul_f32 v[8:9], v[58:59], v[114:115] op_sel:[1,1] op_sel_hi:[0,1] neg_lo:[0,1]
	v_pk_fma_f32 v[118:119], v[58:59], v[114:115], v[8:9] op_sel_hi:[1,0,1]
	v_fmac_f32_e32 v31, v33, v31
	v_pk_mul_f32 v[8:9], v[58:59], v[118:119] op_sel:[1,1] op_sel_hi:[0,1] neg_lo:[0,1]
	v_pk_fma_f32 v[122:123], v[58:59], v[118:119], v[8:9] op_sel_hi:[1,0,1]
	v_div_scale_f32 v33, vcc, s6, v27, s6
	v_pk_mul_f32 v[8:9], v[58:59], v[122:123] op_sel:[1,1] op_sel_hi:[0,1] neg_lo:[0,1]
	v_pk_fma_f32 v[120:121], v[58:59], v[122:123], v[8:9] op_sel_hi:[1,0,1]
	v_mul_f32_e32 v47, v33, v31
	v_pk_mul_f32 v[8:9], v[58:59], v[120:121] op_sel:[1,1] op_sel_hi:[0,1] neg_lo:[0,1]
	v_pk_fma_f32 v[116:117], v[58:59], v[120:121], v[8:9] op_sel_hi:[1,0,1]
	v_fma_f32 v49, -v29, v47, v33
	v_pk_mul_f32 v[8:9], v[58:59], v[116:117] op_sel:[1,1] op_sel_hi:[0,1] neg_lo:[0,1]
	v_pk_fma_f32 v[124:125], v[58:59], v[116:117], v[8:9] op_sel_hi:[1,0,1]
	v_fmac_f32_e32 v47, v49, v31
	v_pk_mul_f32 v[8:9], v[58:59], v[124:125] op_sel:[1,1] op_sel_hi:[0,1] neg_lo:[0,1]
	v_pk_fma_f32 v[126:127], v[58:59], v[124:125], v[8:9] op_sel_hi:[1,0,1]
	v_fma_f32 v29, -v29, v47, v33
	v_pk_mul_f32 v[8:9], v[58:59], v[126:127] op_sel:[1,1] op_sel_hi:[0,1] neg_lo:[0,1]
	v_pk_fma_f32 v[128:129], v[58:59], v[126:127], v[8:9] op_sel_hi:[1,0,1]
	v_div_fmas_f32 v29, v29, v31, v47
	v_pk_mul_f32 v[8:9], v[58:59], v[128:129] op_sel:[1,1] op_sel_hi:[0,1] neg_lo:[0,1]
	v_pk_fma_f32 v[130:131], v[58:59], v[128:129], v[8:9] op_sel_hi:[1,0,1]
	v_div_fixup_f32 v201, v29, v27, s6
	v_pk_mul_f32 v[8:9], v[58:59], v[130:131] op_sel:[1,1] op_sel_hi:[0,1] neg_lo:[0,1]
	v_pk_fma_f32 v[132:133], v[58:59], v[130:131], v[8:9] op_sel_hi:[1,0,1]
	s_mov_b32 s8, 0x3f74fa0b
	v_pk_mul_f32 v[8:9], v[58:59], v[132:133] op_sel:[1,1] op_sel_hi:[0,1] neg_lo:[0,1]
	v_pk_fma_f32 v[134:135], v[58:59], v[132:133], v[8:9] op_sel_hi:[1,0,1]
	s_mov_b32 s10, 0x3f54db31
	v_pk_mul_f32 v[8:9], v[58:59], v[134:135] op_sel:[1,1] op_sel_hi:[0,1] neg_lo:[0,1]
	v_pk_fma_f32 v[136:137], v[58:59], v[134:135], v[8:9] op_sel_hi:[1,0,1]
	s_mov_b32 s14, 0x3f226799
	v_pk_mul_f32 v[8:9], v[58:59], v[136:137] op_sel:[1,1] op_sel_hi:[0,1] neg_lo:[0,1]
	v_pk_fma_f32 v[138:139], v[58:59], v[136:137], v[8:9] op_sel_hi:[1,0,1]
	s_mov_b32 s16, 0x3ef15aea
	v_pk_mul_f32 v[8:9], v[58:59], v[138:139] op_sel:[1,1] op_sel_hi:[0,1] neg_lo:[0,1]
	v_pk_fma_f32 v[140:141], v[58:59], v[138:139], v[8:9] op_sel_hi:[1,0,1]
	s_mov_b32 s18, 0x3e94a031
	v_pk_mul_f32 v[8:9], v[58:59], v[140:141] op_sel:[1,1] op_sel_hi:[0,1] neg_lo:[0,1]
	v_pk_fma_f32 v[142:143], v[58:59], v[140:141], v[8:9] op_sel_hi:[1,0,1]
	s_and_b64 vcc, exec, s[2:3]
	v_pk_mul_f32 v[8:9], v[58:59], v[142:143] op_sel:[1,1] op_sel_hi:[0,1] neg_lo:[0,1]
	v_pk_fma_f32 v[144:145], v[58:59], v[142:143], v[8:9] op_sel_hi:[1,0,1]
	s_movk_i32 s43, 0x4000
	v_pk_mul_f32 v[8:9], v[58:59], v[144:145] op_sel:[1,1] op_sel_hi:[0,1] neg_lo:[0,1]
	v_pk_fma_f32 v[146:147], v[58:59], v[144:145], v[8:9] op_sel_hi:[1,0,1]
	s_movk_i32 s48, 0xfc00
	v_pk_mul_f32 v[8:9], v[58:59], v[146:147] op_sel:[1,1] op_sel_hi:[0,1] neg_lo:[0,1]
	v_pk_fma_f32 v[148:149], v[58:59], v[146:147], v[8:9] op_sel_hi:[1,0,1]
	s_movk_i32 s49, 0xfa00
	v_pk_mul_f32 v[8:9], v[58:59], v[148:149] op_sel:[1,1] op_sel_hi:[0,1] neg_lo:[0,1]
	v_pk_fma_f32 v[150:151], v[58:59], v[148:149], v[8:9] op_sel_hi:[1,0,1]
	s_movk_i32 s50, 0xf800
	v_pk_mul_f32 v[8:9], v[58:59], v[150:151] op_sel:[1,1] op_sel_hi:[0,1] neg_lo:[0,1]
	v_pk_fma_f32 v[152:153], v[58:59], v[150:151], v[8:9] op_sel_hi:[1,0,1]
	s_movk_i32 s51, 0xf600
	v_pk_mul_f32 v[8:9], v[58:59], v[152:153] op_sel:[1,1] op_sel_hi:[0,1] neg_lo:[0,1]
	v_pk_fma_f32 v[154:155], v[58:59], v[152:153], v[8:9] op_sel_hi:[1,0,1]
	s_movk_i32 s57, 0xf400
	v_pk_mul_f32 v[8:9], v[58:59], v[154:155] op_sel:[1,1] op_sel_hi:[0,1] neg_lo:[0,1]
	v_pk_fma_f32 v[156:157], v[58:59], v[154:155], v[8:9] op_sel_hi:[1,0,1]
	s_movk_i32 s58, 0xf200
	v_pk_mul_f32 v[8:9], v[58:59], v[156:157] op_sel:[1,1] op_sel_hi:[0,1] neg_lo:[0,1]
	v_pk_fma_f32 v[8:9], v[58:59], v[156:157], v[8:9] op_sel_hi:[1,0,1]
	v_pk_mul_f32 v[58:59], v[102:103], v[8:9] op_sel:[1,1] op_sel_hi:[0,1] neg_hi:[1,0]
	s_movk_i32 s59, 0xf000
	v_pk_fma_f32 v[8:9], v[102:103], v[8:9], v[58:59] op_sel_hi:[1,0,1]
	v_pk_mul_f32 v[58:59], v[100:101], v[156:157] op_sel:[1,1] op_sel_hi:[0,1] neg_hi:[1,0]
	s_movk_i32 s60, 0xee00
	v_pk_fma_f32 v[58:59], v[100:101], v[156:157], v[58:59] op_sel_hi:[1,0,1]
	v_pk_mul_f32 v[100:101], v[60:61], v[154:155] op_sel:[1,1] op_sel_hi:[0,1] neg_hi:[1,0]
	s_movk_i32 s61, 0xec00
	v_pk_fma_f32 v[60:61], v[60:61], v[154:155], v[100:101] op_sel_hi:[1,0,1]
	v_pk_mul_f32 v[100:101], v[62:63], v[152:153] op_sel:[1,1] op_sel_hi:[0,1] neg_hi:[1,0]
	s_movk_i32 s62, 0xea00
	v_pk_fma_f32 v[62:63], v[62:63], v[152:153], v[100:101] op_sel_hi:[1,0,1]
	v_pk_mul_f32 v[100:101], v[66:67], v[150:151] op_sel:[1,1] op_sel_hi:[0,1] neg_hi:[1,0]
	s_movk_i32 s63, 0xe800
	v_pk_fma_f32 v[66:67], v[66:67], v[150:151], v[100:101] op_sel_hi:[1,0,1]
	v_pk_mul_f32 v[100:101], v[68:69], v[148:149] op_sel:[1,1] op_sel_hi:[0,1] neg_hi:[1,0]
	s_movk_i32 s66, 0xe600
	v_pk_fma_f32 v[68:69], v[68:69], v[148:149], v[100:101] op_sel_hi:[1,0,1]
	v_pk_mul_f32 v[100:101], v[70:71], v[146:147] op_sel:[1,1] op_sel_hi:[0,1] neg_hi:[1,0]
	s_movk_i32 s67, 0xe400
	v_pk_fma_f32 v[70:71], v[70:71], v[146:147], v[100:101] op_sel_hi:[1,0,1]
	v_pk_mul_f32 v[100:101], v[72:73], v[144:145] op_sel:[1,1] op_sel_hi:[0,1] neg_hi:[1,0]
	s_movk_i32 s68, 0xe200
	v_pk_fma_f32 v[72:73], v[72:73], v[144:145], v[100:101] op_sel_hi:[1,0,1]
	v_pk_mul_f32 v[100:101], v[90:91], v[142:143] op_sel:[1,1] op_sel_hi:[0,1] neg_hi:[1,0]
	s_movk_i32 s69, 0xe000
	v_pk_fma_f32 v[90:91], v[90:91], v[142:143], v[100:101] op_sel_hi:[1,0,1]
	v_pk_mul_f32 v[100:101], v[94:95], v[140:141] op_sel:[1,1] op_sel_hi:[0,1] neg_hi:[1,0]
	s_movk_i32 s74, 0xde00
	v_pk_fma_f32 v[94:95], v[94:95], v[140:141], v[100:101] op_sel_hi:[1,0,1]
	v_pk_mul_f32 v[100:101], v[98:99], v[138:139] op_sel:[1,1] op_sel_hi:[0,1] neg_hi:[1,0]
	s_movk_i32 s75, 0xdc00
	v_pk_fma_f32 v[144:145], v[98:99], v[138:139], v[100:101] op_sel_hi:[1,0,1]
	v_pk_mul_f32 v[98:99], v[96:97], v[136:137] op_sel:[1,1] op_sel_hi:[0,1] neg_hi:[1,0]
	s_movk_i32 s79, 0xda00
	v_pk_fma_f32 v[140:141], v[96:97], v[136:137], v[98:99] op_sel_hi:[1,0,1]
	v_pk_mul_f32 v[96:97], v[92:93], v[134:135] op_sel:[1,1] op_sel_hi:[0,1] neg_hi:[1,0]
	s_movk_i32 s56, 0xd800
	v_pk_fma_f32 v[138:139], v[92:93], v[134:135], v[96:97] op_sel_hi:[1,0,1]
	v_pk_mul_f32 v[92:93], v[88:89], v[132:133] op_sel:[1,1] op_sel_hi:[0,1] neg_hi:[1,0]
	s_mov_b32 s9, 0xbe94a031
	v_pk_fma_f32 v[136:137], v[88:89], v[132:133], v[92:93] op_sel_hi:[1,0,1]
	v_pk_mul_f32 v[88:89], v[86:87], v[130:131] op_sel:[1,1] op_sel_hi:[0,1] neg_hi:[1,0]
	s_mov_b32 s11, 0xbf0e39da
	v_pk_fma_f32 v[132:133], v[86:87], v[130:131], v[88:89] op_sel_hi:[1,0,1]
	v_pk_mul_f32 v[86:87], v[84:85], v[128:129] op_sel:[1,1] op_sel_hi:[0,1] neg_hi:[1,0]
	s_mov_b32 s15, 0xbf45e403
	v_pk_fma_f32 v[130:131], v[84:85], v[128:129], v[86:87] op_sel_hi:[1,0,1]
	v_pk_mul_f32 v[84:85], v[82:83], v[126:127] op_sel:[1,1] op_sel_hi:[0,1] neg_hi:[1,0]
	v_mov_b32_e32 v86, v19
	v_pk_fma_f32 v[92:93], v[82:83], v[126:127], v[84:85] op_sel_hi:[1,0,1]
	v_pk_mul_f32 v[82:83], v[80:81], v[124:125] op_sel:[1,1] op_sel_hi:[0,1] neg_hi:[1,0]
	v_pk_mul_f32 v[86:87], v[86:87], s[4:5] op_sel_hi:[0,1] neg_lo:[1,0]
	v_pk_fma_f32 v[96:97], v[80:81], v[124:125], v[82:83] op_sel_hi:[1,0,1]
	v_pk_mul_f32 v[80:81], v[78:79], v[116:117] op_sel:[1,1] op_sel_hi:[0,1] neg_hi:[1,0]
	v_pk_add_f32 v[88:89], v[96:97], v[58:59]
	v_pk_fma_f32 v[116:117], v[78:79], v[116:117], v[80:81] op_sel_hi:[1,0,1]
	v_pk_mul_f32 v[78:79], v[76:77], v[120:121] op_sel:[1,1] op_sel_hi:[0,1] neg_hi:[1,0]
	v_pk_fma_f32 v[86:87], v[16:17], s[44:45], v[86:87] op_sel_hi:[0,1,1]
	v_pk_fma_f32 v[120:121], v[76:77], v[120:121], v[78:79] op_sel_hi:[1,0,1]
	v_pk_mul_f32 v[76:77], v[74:75], v[122:123] op_sel:[1,1] op_sel_hi:[0,1] neg_hi:[1,0]
	v_pk_add_f32 v[78:79], v[92:93], v[8:9]
	v_pk_fma_f32 v[122:123], v[74:75], v[122:123], v[76:77] op_sel_hi:[1,0,1]
	v_pk_mul_f32 v[74:75], v[64:65], v[118:119] op_sel:[1,1] op_sel_hi:[0,1] neg_hi:[1,0]
	s_mov_b64 s[4:5], -1
	v_pk_fma_f32 v[124:125], v[64:65], v[118:119], v[74:75] op_sel_hi:[1,0,1]
	v_pk_mul_f32 v[64:65], v[56:57], v[114:115] op_sel:[1,1] op_sel_hi:[0,1] neg_hi:[1,0]
	s_mov_b32 s17, 0xbf61c598
	v_pk_fma_f32 v[126:127], v[56:57], v[114:115], v[64:65] op_sel_hi:[1,0,1]
	v_pk_mul_f32 v[56:57], v[54:55], v[112:113] op_sel:[1,1] op_sel_hi:[0,1] neg_hi:[1,0]
	v_pk_add_f32 v[118:119], v[126:127], v[70:71]
	v_pk_fma_f32 v[128:129], v[54:55], v[112:113], v[56:57] op_sel_hi:[1,0,1]
	v_pk_mul_f32 v[54:55], v[52:53], v[110:111] op_sel:[1,1] op_sel_hi:[0,1] neg_hi:[1,0]
	v_pk_add_f32 v[114:115], v[128:129], v[72:73]
	v_pk_fma_f32 v[134:135], v[52:53], v[110:111], v[54:55] op_sel_hi:[1,0,1]
	v_pk_mul_f32 v[52:53], v[50:51], v[108:109] op_sel:[1,1] op_sel_hi:[0,1] neg_hi:[1,0]
	v_pk_add_f32 v[64:65], v[134:135], v[90:91]
	v_pk_fma_f32 v[142:143], v[50:51], v[108:109], v[52:53] op_sel_hi:[1,0,1]
	v_pk_mul_f32 v[50:51], v[44:45], v[106:107] op_sel:[1,1] op_sel_hi:[0,1] neg_hi:[1,0]
	v_pk_add_f32 v[74:75], v[142:143], v[94:95]
	v_pk_fma_f32 v[146:147], v[44:45], v[106:107], v[50:51] op_sel_hi:[1,0,1]
	v_pk_mul_f32 v[44:45], v[42:43], v[104:105] op_sel:[1,1] op_sel_hi:[0,1] neg_hi:[1,0]
	v_pk_add_f32 v[76:77], v[146:147], v[144:145]
	v_pk_fma_f32 v[148:149], v[42:43], v[104:105], v[44:45] op_sel_hi:[1,0,1]
	v_pk_mul_f32 v[42:43], v[40:41], v[6:7] op_sel:[1,1] op_sel_hi:[0,1] neg_hi:[1,0]
	v_pk_add_f32 v[80:81], v[148:149], v[140:141]
	v_pk_fma_f32 v[150:151], v[40:41], v[6:7], v[42:43] op_sel_hi:[1,0,1]
	v_pk_mul_f32 v[6:7], v[38:39], v[4:5] op_sel:[1,1] op_sel_hi:[0,1] neg_hi:[1,0]
	v_pk_add_f32 v[104:105], v[150:151], v[138:139]
	v_pk_fma_f32 v[152:153], v[38:39], v[4:5], v[6:7] op_sel_hi:[1,0,1]
	v_pk_mul_f32 v[4:5], v[2:3], v[36:37] op_sel:[1,1] op_sel_hi:[1,0] neg_hi:[0,1]
	v_pk_add_f32 v[102:103], v[152:153], v[136:137]
	v_pk_fma_f32 v[154:155], v[36:37], v[2:3], v[4:5] op_sel_hi:[1,0,1]
	v_pk_fma_f32 v[156:157], v[34:35], 0, v[34:35] op_sel:[1,0,0] op_sel_hi:[0,0,1] neg_hi:[1,0,0]
	v_pk_add_f32 v[100:101], v[154:155], v[132:133]
	v_pk_add_f32 v[98:99], v[156:157], v[130:131]
	v_pk_add_f32 v[112:113], v[124:125], v[68:69]
	v_pk_add_f32 v[110:111], v[122:123], v[66:67]
	v_pk_add_f32 v[106:107], v[120:121], v[62:63]
	v_pk_add_f32 v[108:109], v[116:117], v[60:61]
	v_pk_add_f32 v[40:41], v[98:99], v[114:115]
	v_pk_add_f32 v[42:43], v[100:101], v[118:119]
	v_pk_add_f32 v[36:37], v[102:103], v[112:113]
	v_pk_add_f32 v[34:35], v[104:105], v[110:111]
	v_pk_add_f32 v[82:83], v[80:81], v[106:107]
	v_pk_add_f32 v[84:85], v[76:77], v[108:109]
	v_pk_add_f32 v[44:45], v[74:75], v[88:89]
	v_pk_add_f32 v[38:39], v[64:65], v[78:79]
	v_pk_add_f32 v[50:51], v[40:41], v[82:83]
	v_pk_add_f32 v[52:53], v[42:43], v[84:85]
	v_pk_add_f32 v[54:55], v[36:37], v[44:45]
	v_pk_add_f32 v[56:57], v[34:35], v[38:39]
	v_pk_add_f32 v[4:5], v[50:51], v[54:55]
	v_pk_add_f32 v[6:7], v[52:53], v[56:57]
	s_mov_b32 s19, 0xbf74fa0b
	v_pk_add_f32 v[2:3], v[4:5], v[6:7]
	s_movk_i32 s84, 0xce00
	v_pk_mul_f32 v[2:3], v[86:87], v[2:3]
	v_lshl_add_u64 v[86:87], v[14:15], 1, s[52:53]
	s_nop 0
	v_add_f32_e32 v2, v10, v2
	v_add_f32_e32 v10, v3, v2
	s_nop 0
	v_lshlrev_b32_e32 v2, 16, v25
	v_mul_f32_e32 v2, v198, v2
	v_fmac_f32_e32 v2, v197, v18
	v_fmac_f32_e32 v2, v199, v17
	v_add_f32_e32 v17, v200, v2
	v_lshl_add_u64 v[2:3], v[14:15], 2, s[64:65]
	v_mov_b32_e32 v18, v205
	s_movk_i32 s23, 0xfe00
	s_nop 0
	v_mul_f32_e32 v18, v13, v18
	v_fmac_f32_e32 v18, v201, v10
	v_mul_f32_e32 v10, v17, v18
	s_cbranch_vccz .LBB0_640
	v_bfe_u32 v15, v10, 16, 1
	s_movk_i32 s4, 0x7fff
	v_add3_u32 v15, v10, v15, s4
	global_store_short_d16_hi v[86:87], v15, off
	s_mov_b64 s[4:5], 0

.LBB0_646:
	s_or_b64 exec, exec, s[4:5]
	v_pk_add_f32 v[136:137], v[152:153], v[136:137] neg_lo:[0,1] neg_hi:[0,1]
	v_pk_add_f32 v[140:141], v[148:149], v[140:141] neg_lo:[0,1] neg_hi:[0,1]
	s_nop 0
	v_pk_mul_f32 v[152:153], v[30:31], v[136:137] op_sel:[0,1] op_sel_hi:[0,0] neg_lo:[0,1]
	v_pk_fma_f32 v[136:137], v[32:33], v[136:137], v[152:153] op_sel_hi:[0,1,1]
	v_mov_b32_e32 v33, v210
	v_pk_add_f32 v[72:73], v[128:129], v[72:73] neg_lo:[0,1] neg_hi:[0,1]
	v_pk_add_f32 v[70:71], v[126:127], v[70:71] neg_lo:[0,1] neg_hi:[0,1]
	v_pk_add_f32 v[90:91], v[134:135], v[90:91] neg_lo:[0,1] neg_hi:[0,1]
	v_xor_b32_e32 v134, 0x80000000, v73
	v_mov_b32_e32 v135, v72
	v_pk_mul_f32 v[148:149], v[46:47], v[140:141] op_sel:[0,1] op_sel_hi:[0,0] neg_lo:[0,1]
	v_pk_mul_f32 v[72:73], v[24:25], v[70:71] op_sel:[0,1] op_sel_hi:[0,0] neg_lo:[0,1]
	v_pk_add_f32 v[68:69], v[124:125], v[68:69] neg_lo:[0,1] neg_hi:[0,1]
	v_pk_fma_f32 v[140:141], v[46:47], v[140:141], v[148:149] op_sel_hi:[0,1,1]
	v_pk_fma_f32 v[148:149], v[26:27], v[70:71], v[72:73] op_sel_hi:[0,1,1] neg_lo:[1,0,0] neg_hi:[1,0,0]
	v_pk_add_f32 v[138:139], v[150:151], v[138:139] neg_lo:[0,1] neg_hi:[0,1]
	v_pk_add_f32 v[66:67], v[122:123], v[66:67] neg_lo:[0,1] neg_hi:[0,1]
	v_pk_mul_f32 v[150:151], v[48:49], v[138:139] op_sel:[0,1] op_sel_hi:[0,0] neg_lo:[0,1]
	v_pk_add_f32 v[62:63], v[120:121], v[62:63] neg_lo:[0,1] neg_hi:[0,1]
	v_pk_fma_f32 v[138:139], v[28:29], v[138:139], v[150:151] op_sel_hi:[0,1,1]
	v_pk_add_f32 v[144:145], v[146:147], v[144:145] neg_lo:[0,1] neg_hi:[0,1]
	v_pk_add_f32 v[132:133], v[154:155], v[132:133] neg_lo:[0,1] neg_hi:[0,1]
	v_pk_add_f32 v[60:61], v[116:117], v[60:61] neg_lo:[0,1] neg_hi:[0,1]
	v_pk_mul_f32 v[146:147], v[28:29], v[144:145] op_sel:[0,1] op_sel_hi:[0,0] neg_lo:[0,1]
	v_pk_mul_f32 v[154:155], v[26:27], v[132:133] op_sel:[0,1] op_sel_hi:[0,0] neg_lo:[0,1]
	v_pk_fma_f32 v[144:145], v[48:49], v[144:145], v[146:147] op_sel_hi:[0,1,1]
	v_pk_add_f32 v[94:95], v[142:143], v[94:95] neg_lo:[0,1] neg_hi:[0,1]
	v_pk_fma_f32 v[132:133], v[24:25], v[132:133], v[154:155] op_sel_hi:[0,1,1]
	v_pk_add_f32 v[8:9], v[92:93], v[8:9] neg_lo:[0,1] neg_hi:[0,1]
	v_pk_add_f32 v[130:131], v[156:157], v[130:131] neg_lo:[0,1] neg_hi:[0,1]
	v_pk_add_f32 v[92:93], v[132:133], v[148:149]
	v_xor_b32_e32 v18, 0x80000000, v19
	s_mov_b32 s4, s41
	s_mov_b32 s5, s40
	v_mov_b32_e32 v17, v16
	s_andn2_b64 vcc, exec, s[2:3]
	s_nop 0
	v_pk_mul_f32 v[70:71], v[32:33], v[68:69] op_sel:[0,1] op_sel_hi:[0,0] neg_lo:[0,1]
	v_pk_fma_f32 v[124:125], v[30:31], v[68:69], v[70:71] op_sel_hi:[0,1,1] neg_lo:[1,0,0] neg_hi:[1,0,0]
	v_pk_mul_f32 v[68:69], v[28:29], v[66:67] op_sel:[0,1] op_sel_hi:[0,0] neg_lo:[0,1]
	v_pk_fma_f32 v[150:151], v[48:49], v[66:67], v[68:69] op_sel_hi:[0,1,1] neg_lo:[1,0,0] neg_hi:[1,0,0]
	v_pk_mul_f32 v[66:67], v[46:47], v[62:63] op_sel:[0,1] op_sel_hi:[0,0] neg_lo:[0,1]
	v_pk_fma_f32 v[152:153], v[46:47], v[62:63], v[66:67] op_sel_hi:[0,1,1] neg_lo:[1,0,0] neg_hi:[1,0,0]
	v_xor_b32_e32 v62, 0x80000000, v61
	v_mov_b32_e32 v63, v60
	v_pk_mul_f32 v[48:49], v[48:49], v[62:63] op_sel_hi:[0,1]
	v_pk_fma_f32 v[154:155], v[28:29], v[60:61], v[48:49] op_sel_hi:[0,1,1] neg_lo:[1,0,0] neg_hi:[1,0,0]
	v_pk_add_f32 v[28:29], v[96:97], v[58:59] neg_lo:[0,1] neg_hi:[0,1]
	v_pk_mul_f32 v[142:143], v[32:33], v[94:95] op_sel:[0,1] op_sel_hi:[0,0] neg_lo:[0,1]
	v_pk_fma_f32 v[142:143], v[30:31], v[94:95], v[142:143] op_sel_hi:[0,1,1]
	v_pk_mul_f32 v[48:49], v[30:31], v[28:29] op_sel:[0,1] op_sel_hi:[0,0] neg_lo:[0,1]
	v_pk_mul_f32 v[94:95], v[24:25], v[90:91] op_sel:[0,1] op_sel_hi:[0,0] neg_lo:[0,1]
	v_pk_fma_f32 v[156:157], v[32:33], v[28:29], v[48:49] op_sel_hi:[0,1,1] neg_lo:[1,0,0] neg_hi:[1,0,0]
	v_pk_fma_f32 v[146:147], v[26:27], v[90:91], v[94:95] op_sel_hi:[0,1,1]
	v_pk_mul_f32 v[26:27], v[26:27], v[8:9] op_sel:[0,1] op_sel_hi:[0,0] neg_lo:[0,1]
	v_pk_fma_f32 v[158:159], v[24:25], v[8:9], v[26:27] op_sel_hi:[0,1,1] neg_lo:[1,0,0] neg_hi:[1,0,0]
	v_pk_add_f32 v[90:91], v[130:131], v[134:135]
	v_pk_add_f32 v[94:95], v[136:137], v[124:125]
	v_pk_add_f32 v[96:97], v[138:139], v[150:151]
	v_pk_add_f32 v[126:127], v[140:141], v[152:153]
	v_pk_add_f32 v[128:129], v[144:145], v[154:155]
	v_pk_add_f32 v[122:123], v[142:143], v[156:157]
	v_pk_add_f32 v[116:117], v[146:147], v[158:159]
	v_pk_add_f32 v[66:67], v[90:91], v[126:127]
	v_pk_add_f32 v[68:69], v[92:93], v[128:129]
	v_pk_add_f32 v[70:71], v[94:95], v[122:123]
	v_pk_add_f32 v[72:73], v[96:97], v[116:117]
	v_pk_add_f32 v[26:27], v[66:67], v[70:71]
	v_pk_add_f32 v[28:29], v[68:69], v[72:73]
	v_pk_mul_f32 v[48:49], v[18:19], s[4:5]
	v_pk_add_f32 v[8:9], v[26:27], v[28:29]
	v_pk_fma_f32 v[48:49], v[16:17], s[40:41], v[48:49]
	v_pk_mul_f32 v[8:9], v[48:49], v[8:9]
	v_add_f32_e32 v8, v8, v25
	v_add_f32_e32 v8, v9, v8
	v_lshlrev_b32_e32 v9, 16, v31
	v_mul_f32_e32 v9, v198, v9
	v_fmac_f32_e32 v9, v197, v10
	v_fmac_f32_e32 v9, v199, v15
	v_mul_f32_e32 v10, v13, v33
	v_add_f32_e32 v9, v200, v9
	v_fmac_f32_e32 v10, v201, v8
	v_mul_f32_e32 v8, v9, v10
	v_cndmask_b32_e64 v9, 0, 1, s[2:3]
	v_cmp_ne_u32_e64 s[4:5], 1, v9
	s_mov_b64 s[2:3], -1
	s_cbranch_vccnz .LBB0_648
	v_bfe_u32 v9, v8, 16, 1
	s_movk_i32 s2, 0x7fff
	v_add3_u32 v9, v8, v9, s2
	s_mov_b64 s[2:3], 0
	global_store_short_d16_hi v[86:87], v9, off offset:1024

.LBB0_654:
	s_or_b64 exec, exec, s[2:3]
	v_pk_add_f32 v[8:9], v[100:101], v[118:119] neg_lo:[0,1] neg_hi:[0,1]
	v_mov_b32_e32 v31, v30
	v_mov_b32_e32 v33, v32
	v_pk_mul_f32 v[24:25], v[30:31], v[8:9] op_sel:[0,1] op_sel_hi:[1,0] neg_lo:[0,1]
	v_mov_b32_e32 v47, v46
	v_pk_fma_f32 v[100:101], v[32:33], v[8:9], v[24:25]
	v_pk_add_f32 v[8:9], v[102:103], v[112:113] neg_lo:[0,1] neg_hi:[0,1]
	v_xor_b32_e32 v162, 0x80000000, v30
	v_pk_mul_f32 v[24:25], v[46:47], v[8:9] op_sel:[0,1] op_sel_hi:[1,0] neg_lo:[0,1]
	v_mov_b32_e32 v163, v162
	v_pk_fma_f32 v[102:103], v[46:47], v[8:9], v[24:25]
	v_pk_add_f32 v[8:9], v[104:105], v[110:111] neg_lo:[0,1] neg_hi:[0,1]
	v_xor_b32_e32 v48, 0x80000000, v46
	v_pk_mul_f32 v[24:25], v[32:33], v[8:9] op_sel:[0,1] op_sel_hi:[1,0] neg_lo:[0,1]
	v_mov_b32_e32 v49, v48
	v_pk_fma_f32 v[104:105], v[30:31], v[8:9], v[24:25]
	v_pk_add_f32 v[8:9], v[80:81], v[106:107] neg_lo:[0,1] neg_hi:[0,1]
	v_xor_b32_e32 v160, 0x80000000, v32
	v_xor_b32_e32 v106, 0x80000000, v9
	v_mov_b32_e32 v107, v8
	v_pk_add_f32 v[8:9], v[76:77], v[108:109] neg_lo:[0,1] neg_hi:[0,1]
	v_mov_b32_e32 v161, v160
	v_pk_mul_f32 v[24:25], v[32:33], v[8:9] op_sel:[0,1] op_sel_hi:[1,0] neg_lo:[0,1]
	v_pk_add_f32 v[98:99], v[98:99], v[114:115] neg_lo:[0,1] neg_hi:[0,1]
	v_pk_fma_f32 v[108:109], v[162:163], v[8:9], v[24:25]
	v_pk_add_f32 v[8:9], v[74:75], v[88:89] neg_lo:[0,1] neg_hi:[0,1]
	v_pk_add_f32 v[58:59], v[98:99], v[106:107]
	v_pk_mul_f32 v[24:25], v[46:47], v[8:9] op_sel:[0,1] op_sel_hi:[1,0] neg_lo:[0,1]
	v_pk_add_f32 v[60:61], v[100:101], v[108:109]
	v_pk_fma_f32 v[110:111], v[48:49], v[8:9], v[24:25]
	v_pk_add_f32 v[8:9], v[64:65], v[78:79] neg_lo:[0,1] neg_hi:[0,1]
	v_pk_add_f32 v[62:63], v[102:103], v[110:111]
	v_pk_mul_f32 v[24:25], v[30:31], v[8:9] op_sel:[0,1] op_sel_hi:[1,0] neg_lo:[0,1]
	s_mov_b32 s2, s77
	v_pk_fma_f32 v[112:113], v[160:161], v[8:9], v[24:25]
	s_mov_b32 s3, s76
	v_pk_add_f32 v[64:65], v[104:105], v[112:113]
	v_pk_add_f32 v[8:9], v[58:59], v[62:63]
	v_pk_add_f32 v[24:25], v[60:61], v[64:65]
	v_pk_mul_f32 v[76:77], v[18:19], s[2:3]
	v_pk_add_f32 v[74:75], v[8:9], v[24:25]
	v_pk_fma_f32 v[76:77], v[16:17], s[76:77], v[76:77]
	s_mov_b64 s[2:3], -1
	v_pk_mul_f32 v[74:75], v[76:77], v[74:75]
	v_add_f32_e32 v74, v74, v120
	v_add_f32_e32 v76, v75, v74
	s_nop 0
	v_lshlrev_b32_e32 v74, 16, v121
	v_mul_f32_e32 v74, v198, v74
	v_fmac_f32_e32 v74, v197, v10
	v_fmac_f32_e32 v74, v199, v15
	v_add_f32_e32 v10, v200, v74
	v_add_co_u32_e32 v74, vcc, 0x1000, v2
	s_nop 1
	v_addc_co_u32_e32 v75, vcc, 0, v3, vcc
	v_mov_b32_e32 v15, v215
	s_and_b64 vcc, exec, s[4:5]
	s_nop 0
	v_mul_f32_e32 v15, v13, v15
	v_fmac_f32_e32 v15, v201, v76
	v_mul_f32_e32 v10, v10, v15
	s_cbranch_vccnz .LBB0_656
	v_bfe_u32 v15, v10, 16, 1
	s_movk_i32 s2, 0x7fff
	v_add3_u32 v15, v10, v15, s2
	s_mov_b64 s[2:3], 0
	global_store_short_d16_hi v[86:87], v15, off offset:2048

.LBB0_662:
	s_or_b64 exec, exec, s[2:3]
	v_pk_add_f32 v[74:75], v[132:133], v[148:149] neg_lo:[0,1] neg_hi:[0,1]
	v_pk_add_f32 v[114:115], v[130:131], v[134:135] neg_lo:[0,1] neg_hi:[0,1]
	v_pk_mul_f32 v[76:77], v[30:31], v[74:75] op_sel:[0,1] op_sel_hi:[1,0] neg_lo:[0,1]
	s_mov_b32 s2, s9
	v_pk_fma_f32 v[118:119], v[32:33], v[74:75], v[76:77]
	v_pk_add_f32 v[74:75], v[136:137], v[124:125] neg_lo:[0,1] neg_hi:[0,1]
	s_mov_b32 s3, s8
	v_pk_mul_f32 v[76:77], v[46:47], v[74:75] op_sel:[0,1] op_sel_hi:[1,0] neg_lo:[0,1]
	v_pk_fma_f32 v[120:121], v[46:47], v[74:75], v[76:77]
	v_pk_add_f32 v[74:75], v[138:139], v[150:151] neg_lo:[0,1] neg_hi:[0,1]
	v_pk_mul_f32 v[76:77], v[32:33], v[74:75] op_sel:[0,1] op_sel_hi:[1,0] neg_lo:[0,1]
	v_pk_fma_f32 v[124:125], v[30:31], v[74:75], v[76:77]
	v_pk_add_f32 v[74:75], v[140:141], v[152:153] neg_lo:[0,1] neg_hi:[0,1]
	v_pk_mul_f32 v[140:141], v[18:19], s[2:3]
	v_xor_b32_e32 v130, 0x80000000, v75
	v_mov_b32_e32 v131, v74
	v_pk_add_f32 v[74:75], v[144:145], v[154:155] neg_lo:[0,1] neg_hi:[0,1]
	v_pk_fma_f32 v[140:141], v[16:17], s[8:9], v[140:141]
	v_pk_mul_f32 v[32:33], v[32:33], v[74:75] op_sel:[0,1] op_sel_hi:[1,0] neg_lo:[0,1]
	s_mov_b64 s[2:3], -1
	v_pk_fma_f32 v[132:133], v[162:163], v[74:75], v[32:33]
	v_pk_add_f32 v[32:33], v[142:143], v[156:157] neg_lo:[0,1] neg_hi:[0,1]
	v_pk_add_f32 v[76:77], v[118:119], v[132:133]
	v_pk_mul_f32 v[74:75], v[46:47], v[32:33] op_sel:[0,1] op_sel_hi:[1,0] neg_lo:[0,1]
	v_pk_fma_f32 v[134:135], v[48:49], v[32:33], v[74:75]
	v_pk_add_f32 v[32:33], v[146:147], v[158:159] neg_lo:[0,1] neg_hi:[0,1]
	v_pk_add_f32 v[78:79], v[120:121], v[134:135]
	v_pk_mul_f32 v[30:31], v[30:31], v[32:33] op_sel:[0,1] op_sel_hi:[1,0] neg_lo:[0,1]
	v_pk_add_f32 v[74:75], v[114:115], v[130:131]
	v_pk_fma_f32 v[136:137], v[160:161], v[32:33], v[30:31]
	v_pk_add_f32 v[30:31], v[74:75], v[78:79]
	v_pk_add_f32 v[80:81], v[124:125], v[136:137]
	v_pk_add_f32 v[32:33], v[76:77], v[80:81]
	v_pk_add_f32 v[138:139], v[30:31], v[32:33]
	v_pk_mul_f32 v[138:139], v[140:141], v[138:139]
	v_add_f32_e32 v88, v138, v88
	v_add_f32_e32 v138, v139, v88
	s_nop 0
	v_lshlrev_b32_e32 v88, 16, v89
	v_mul_f32_e32 v88, v198, v88
	v_fmac_f32_e32 v88, v197, v10
	v_fmac_f32_e32 v88, v199, v15
	v_add_f32_e32 v10, v200, v88
	v_add_co_u32_e32 v88, vcc, 0x1000, v2
	s_nop 1
	v_addc_co_u32_e32 v89, vcc, 0, v3, vcc
	v_mov_b32_e32 v15, v220
	s_and_b64 vcc, exec, s[4:5]
	s_nop 0
	v_mul_f32_e32 v15, v13, v15
	v_fmac_f32_e32 v15, v201, v138
	v_mul_f32_e32 v10, v10, v15
	s_cbranch_vccnz .LBB0_664
	v_bfe_u32 v15, v10, 16, 1
	s_movk_i32 s2, 0x7fff
	v_add3_u32 v15, v10, v15, s2
	s_mov_b64 s[2:3], 0
	global_store_short_d16_hi v[86:87], v15, off offset:3072

.LBB0_670:
	s_or_b64 exec, exec, s[2:3]
	v_pk_add_f32 v[82:83], v[40:41], v[82:83] neg_lo:[0,1] neg_hi:[0,1]
	v_pk_add_f32 v[40:41], v[42:43], v[84:85] neg_lo:[0,1] neg_hi:[0,1]
	v_pk_add_f32 v[36:37], v[36:37], v[44:45] neg_lo:[0,1] neg_hi:[0,1]
	v_pk_add_f32 v[34:35], v[34:35], v[38:39] neg_lo:[0,1] neg_hi:[0,1]
	v_xor_b32_e32 v86, 0x80000000, v37
	v_mov_b32_e32 v87, v36
	v_pk_mul_f32 v[42:43], v[46:47], v[40:41] op_sel:[0,1] op_sel_hi:[1,0] neg_lo:[0,1]
	v_pk_mul_f32 v[36:37], v[46:47], v[34:35] op_sel:[0,1] op_sel_hi:[1,0] neg_lo:[0,1]
	v_pk_fma_f32 v[84:85], v[46:47], v[40:41], v[42:43]
	v_pk_fma_f32 v[88:89], v[48:49], v[34:35], v[36:37]
	s_mov_b32 s2, s55
	s_mov_b32 s3, s54
	v_pk_add_f32 v[34:35], v[82:83], v[86:87]
	v_pk_add_f32 v[36:37], v[84:85], v[88:89]
	v_pk_mul_f32 v[40:41], v[18:19], s[2:3]
	v_pk_add_f32 v[38:39], v[34:35], v[36:37]
	v_pk_fma_f32 v[40:41], v[16:17], s[54:55], v[40:41]
	s_mov_b64 s[2:3], -1
	v_pk_mul_f32 v[38:39], v[40:41], v[38:39]
	v_add_f32_e32 v10, v38, v10
	s_nop 0
	v_lshlrev_b32_e32 v38, 16, v141
	v_mul_f32_e32 v38, v198, v38
	v_fmac_f32_e32 v38, v197, v140
	v_fmac_f32_e32 v38, v199, v15
	v_add_f32_e32 v15, v200, v38
	v_add_co_u32_e32 v38, vcc, 0x2000, v2
	v_add_f32_e32 v10, v39, v10
	s_nop 0
	v_addc_co_u32_e32 v39, vcc, 0, v3, vcc
	v_mov_b32_e32 v38, v225
	s_and_b64 vcc, exec, s[4:5]
	s_nop 0
	v_mul_f32_e32 v38, v13, v38
	v_fmac_f32_e32 v38, v201, v10
	v_mul_f32_e32 v10, v15, v38
	s_cbranch_vccnz .LBB0_672
	v_bfe_u32 v15, v10, 16, 1
	s_movk_i32 s2, 0x7fff
	v_add3_u32 v15, v10, v15, s2
	v_lshl_add_u64 v[38:39], v[138:139], 1, s[52:53]
	s_mov_b64 s[2:3], 0
	global_store_short_d16_hi v[38:39], v15, off

.LBB0_686:
	s_or_b64 exec, exec, s[2:3]
	v_pk_add_f32 v[42:43], v[100:101], v[108:109] neg_lo:[0,1] neg_hi:[0,1]
	v_pk_add_f32 v[98:99], v[98:99], v[106:107] neg_lo:[0,1] neg_hi:[0,1]
	v_pk_mul_f32 v[44:45], v[46:47], v[42:43] op_sel:[0,1] op_sel_hi:[1,0] neg_lo:[0,1]
	s_mov_b32 s2, s11
	v_pk_fma_f32 v[100:101], v[46:47], v[42:43], v[44:45]
	v_pk_add_f32 v[42:43], v[102:103], v[110:111] neg_lo:[0,1] neg_hi:[0,1]
	s_mov_b32 s3, s10
	v_xor_b32_e32 v102, 0x80000000, v43
	v_mov_b32_e32 v103, v42
	v_pk_add_f32 v[42:43], v[104:105], v[112:113] neg_lo:[0,1] neg_hi:[0,1]
	v_pk_mul_f32 v[108:109], v[18:19], s[2:3]
	v_pk_mul_f32 v[44:45], v[46:47], v[42:43] op_sel:[0,1] op_sel_hi:[1,0] neg_lo:[0,1]
	v_pk_fma_f32 v[108:109], v[16:17], s[10:11], v[108:109]
	v_pk_fma_f32 v[104:105], v[48:49], v[42:43], v[44:45]
	v_pk_add_f32 v[42:43], v[98:99], v[102:103]
	v_pk_add_f32 v[44:45], v[100:101], v[104:105]
	s_mov_b64 s[2:3], -1
	v_pk_add_f32 v[106:107], v[42:43], v[44:45]
	v_pk_mul_f32 v[106:107], v[108:109], v[106:107]
	v_add_f32_e32 v10, v106, v10
	s_nop 0
	v_lshlrev_b32_e32 v106, 16, v123
	v_mul_f32_e32 v106, v198, v106
	v_fmac_f32_e32 v106, v197, v122
	v_fmac_f32_e32 v106, v199, v15
	v_add_f32_e32 v15, v200, v106
	v_add_co_u32_e32 v106, vcc, 0x3000, v2
	v_add_f32_e32 v10, v107, v10
	s_nop 0
	v_addc_co_u32_e32 v107, vcc, 0, v3, vcc
	v_mov_b32_e32 v106, v235
	s_and_b64 vcc, exec, s[4:5]
	s_nop 0
	v_mul_f32_e32 v106, v13, v106
	v_fmac_f32_e32 v106, v201, v10
	v_mul_f32_e32 v10, v15, v106
	s_cbranch_vccnz .LBB0_688
	v_bfe_u32 v15, v10, 16, 1
	s_movk_i32 s2, 0x7fff
	v_add3_u32 v15, v10, v15, s2
	v_lshl_add_u64 v[106:107], v[116:117], 1, s[52:53]
	s_mov_b64 s[2:3], 0
	global_store_short_d16_hi v[106:107], v15, off

.LBB0_694:
	s_or_b64 exec, exec, s[2:3]
	v_pk_add_f32 v[108:109], v[118:119], v[132:133] neg_lo:[0,1] neg_hi:[0,1]
	v_pk_add_f32 v[112:113], v[120:121], v[134:135] neg_lo:[0,1] neg_hi:[0,1]
	v_pk_mul_f32 v[110:111], v[46:47], v[108:109] op_sel:[0,1] op_sel_hi:[1,0] neg_lo:[0,1]
	v_pk_add_f32 v[106:107], v[114:115], v[130:131] neg_lo:[0,1] neg_hi:[0,1]
	v_pk_fma_f32 v[108:109], v[46:47], v[108:109], v[110:111]
	v_xor_b32_e32 v110, 0x80000000, v113
	v_mov_b32_e32 v111, v112
	v_pk_add_f32 v[112:113], v[124:125], v[136:137] neg_lo:[0,1] neg_hi:[0,1]
	s_mov_b32 s2, s83
	v_pk_mul_f32 v[46:47], v[46:47], v[112:113] op_sel:[0,1] op_sel_hi:[1,0] neg_lo:[0,1]
	s_mov_b32 s3, s82
	v_pk_fma_f32 v[112:113], v[48:49], v[112:113], v[46:47]
	v_pk_add_f32 v[46:47], v[106:107], v[110:111]
	v_pk_add_f32 v[48:49], v[108:109], v[112:113]
	v_pk_mul_f32 v[118:119], v[18:19], s[2:3]
	v_pk_add_f32 v[114:115], v[46:47], v[48:49]
	v_pk_fma_f32 v[118:119], v[16:17], s[82:83], v[118:119]
	s_mov_b64 s[2:3], -1
	v_pk_mul_f32 v[114:115], v[118:119], v[114:115]
	v_add_f32_e32 v10, v114, v10
	s_nop 0
	v_lshlrev_b32_e32 v114, 16, v123
	v_mul_f32_e32 v114, v198, v114
	v_fmac_f32_e32 v114, v197, v122
	v_fmac_f32_e32 v114, v199, v15
	v_add_f32_e32 v15, v200, v114
	v_add_co_u32_e32 v114, vcc, 0x3000, v2
	v_add_f32_e32 v10, v115, v10
	s_nop 0
	v_addc_co_u32_e32 v115, vcc, 0, v3, vcc
	v_mov_b32_e32 v114, v240
	s_and_b64 vcc, exec, s[4:5]
	s_nop 0
	v_mul_f32_e32 v114, v13, v114
	v_fmac_f32_e32 v114, v201, v10
	v_mul_f32_e32 v10, v15, v114
	s_cbranch_vccnz .LBB0_696
	v_bfe_u32 v15, v10, 16, 1
	s_movk_i32 s2, 0x7fff
	v_add3_u32 v15, v10, v15, s2
	v_lshl_add_u64 v[114:115], v[116:117], 1, s[52:53]
	s_mov_b64 s[2:3], 0
	global_store_short_d16_hi v[114:115], v15, off

.LBB0_710:
	s_or_b64 exec, exec, s[2:3]
	v_pk_add_f32 v[54:55], v[66:67], v[70:71] neg_lo:[0,1] neg_hi:[0,1]
	v_pk_add_f32 v[66:67], v[68:69], v[72:73] neg_lo:[0,1] neg_hi:[0,1]
	s_mov_b32 s2, s15
	s_mov_b32 s3, s14
	v_xor_b32_e32 v56, 0x80000000, v67
	v_mov_b32_e32 v57, v66
	v_pk_mul_f32 v[68:69], v[18:19], s[2:3]
	v_pk_add_f32 v[66:67], v[54:55], v[56:57]
	v_pk_fma_f32 v[68:69], v[16:17], s[14:15], v[68:69]
	s_mov_b64 s[2:3], -1
	v_pk_mul_f32 v[66:67], v[68:69], v[66:67]
	v_add_f32_e32 v10, v66, v10
	s_nop 0
	v_lshlrev_b32_e32 v66, 16, v117
	v_mul_f32_e32 v66, v198, v66
	v_fmac_f32_e32 v66, v197, v116
	v_fmac_f32_e32 v66, v199, v15
	v_add_f32_e32 v15, v200, v66
	v_add_co_u32_e32 v66, vcc, 0x4000, v2
	v_add_f32_e32 v10, v67, v10
	s_nop 0
	v_addc_co_u32_e32 v67, vcc, 0, v3, vcc
	v_mov_b32_e32 v66, v210
	s_and_b64 vcc, exec, s[4:5]
	s_nop 0
	v_mul_f32_e32 v66, v13, v66
	v_fmac_f32_e32 v66, v201, v10
	v_mul_f32_e32 v10, v15, v66
	s_cbranch_vccnz .LBB0_712
	v_bfe_u32 v15, v10, 16, 1
	s_movk_i32 s2, 0x7fff
	v_add3_u32 v15, v10, v15, s2
	v_lshl_add_u64 v[66:67], v[114:115], 1, s[52:53]
	s_mov_b64 s[2:3], 0
	global_store_short_d16_hi v[66:67], v15, off

.LBB0_718:
	s_or_b64 exec, exec, s[2:3]
	v_pk_add_f32 v[58:59], v[58:59], v[62:63] neg_lo:[0,1] neg_hi:[0,1]
	v_pk_add_f32 v[62:63], v[60:61], v[64:65] neg_lo:[0,1] neg_hi:[0,1]
	s_mov_b32 s2, s87
	s_mov_b32 s3, s86
	v_xor_b32_e32 v60, 0x80000000, v63
	v_mov_b32_e32 v61, v62
	v_pk_mul_f32 v[64:65], v[18:19], s[2:3]
	v_pk_add_f32 v[62:63], v[58:59], v[60:61]
	v_pk_fma_f32 v[64:65], v[16:17], s[86:87], v[64:65]
	s_mov_b64 s[2:3], -1
	v_pk_mul_f32 v[62:63], v[64:65], v[62:63]
	v_add_f32_e32 v10, v62, v10
	s_nop 0
	v_lshlrev_b32_e32 v62, 16, v69
	v_mul_f32_e32 v62, v198, v62
	v_fmac_f32_e32 v62, v197, v68
	v_fmac_f32_e32 v62, v199, v15
	v_add_f32_e32 v15, v200, v62
	v_add_co_u32_e32 v62, vcc, 0x5000, v2
	v_add_f32_e32 v10, v63, v10
	s_nop 0
	v_addc_co_u32_e32 v63, vcc, 0, v3, vcc
	v_mov_b32_e32 v62, v215
	s_and_b64 vcc, exec, s[4:5]
	s_nop 0
	v_mul_f32_e32 v62, v13, v62
	v_fmac_f32_e32 v62, v201, v10
	v_mul_f32_e32 v10, v15, v62
	s_cbranch_vccnz .LBB0_720
	v_bfe_u32 v15, v10, 16, 1
	s_movk_i32 s2, 0x7fff
	v_add3_u32 v15, v10, v15, s2
	v_lshl_add_u64 v[62:63], v[66:67], 1, s[52:53]
	s_mov_b64 s[2:3], 0
	global_store_short_d16_hi v[62:63], v15, off

.LBB0_766:
	s_or_b64 exec, exec, s[2:3]
	s_mov_b32 s2, s97
	s_mov_b32 s3, s95
	v_pk_add_f32 v[4:5], v[4:5], v[6:7] neg_lo:[0,1] neg_hi:[0,1]
	s_mov_b32 s96, s95
	v_pk_mul_f32 v[6:7], v[18:19], s[2:3]
	s_mov_b64 s[2:3], -1
	v_pk_fma_f32 v[6:7], v[16:17], s[96:97], v[6:7]
	v_pk_mul_f32 v[4:5], v[6:7], v[4:5]
	v_add_f32_e32 v4, v4, v10
	v_add_f32_e32 v6, v5, v4
	s_nop 0
	v_lshlrev_b32_e32 v4, 16, v85
	v_mul_f32_e32 v4, v198, v4
	v_fmac_f32_e32 v4, v197, v84
	v_fmac_f32_e32 v4, v199, v15
	v_add_f32_e32 v7, v200, v4
	v_add_co_u32_e32 v4, vcc, 0x8000, v2
	s_nop 1
	v_addc_co_u32_e32 v5, vcc, 0, v3, vcc
	v_mov_b32_e32 v4, v205
	s_and_b64 vcc, exec, s[4:5]
	s_nop 0
	v_mul_f32_e32 v4, v13, v4
	v_fmac_f32_e32 v4, v201, v6
	v_mul_f32_e32 v4, v7, v4
	s_cbranch_vccnz .LBB0_768
	v_bfe_u32 v5, v4, 16, 1
	s_movk_i32 s2, 0x7fff
	v_add3_u32 v5, v4, v5, s2
	v_lshl_add_u64 v[6:7], v[82:83], 1, s[52:53]
	s_mov_b64 s[2:3], 0
	global_store_short_d16_hi v[6:7], v5, off

.LBB0_774:
	s_or_b64 exec, exec, s[2:3]
	s_mov_b32 s6, s31
	s_mov_b32 s7, s41
	v_pk_add_f32 v[26:27], v[26:27], v[28:29] neg_lo:[0,1] neg_hi:[0,1]
	s_mov_b32 s2, s41
	s_mov_b32 s3, s31
	v_pk_mul_f32 v[28:29], v[18:19], s[6:7]
	v_pk_fma_f32 v[28:29], v[16:17], s[2:3], v[28:29]
	s_mov_b64 s[2:3], -1
	v_pk_mul_f32 v[26:27], v[28:29], v[26:27]
	v_add_f32_e32 v6, v26, v6
	v_add_f32_e32 v26, v27, v6
	s_nop 0
	v_lshlrev_b32_e32 v6, 16, v15
	v_mul_f32_e32 v6, v198, v6
	v_fmac_f32_e32 v6, v197, v10
	v_fmac_f32_e32 v6, v199, v7
	v_add_f32_e32 v10, v200, v6
	v_add_co_u32_e32 v6, vcc, 0x8000, v2
	s_nop 1
	v_addc_co_u32_e32 v7, vcc, 0, v3, vcc
	v_mov_b32_e32 v6, v210
	s_and_b64 vcc, exec, s[4:5]
	s_nop 0
	v_mul_f32_e32 v6, v13, v6
	v_fmac_f32_e32 v6, v201, v26
	v_mul_f32_e32 v6, v10, v6
	s_cbranch_vccnz .LBB0_776
	v_bfe_u32 v7, v6, 16, 1
	s_movk_i32 s2, 0x7fff
	v_add3_u32 v7, v6, v7, s2
	v_lshl_add_u64 v[4:5], v[4:5], 1, s[52:53]
	s_mov_b64 s[2:3], 0
	global_store_short_d16_hi v[4:5], v7, off

.LBB0_782:
	s_or_b64 exec, exec, s[2:3]
	s_mov_b32 s6, s93
	s_mov_b32 s7, s77
	v_pk_add_f32 v[8:9], v[8:9], v[24:25] neg_lo:[0,1] neg_hi:[0,1]
	s_mov_b32 s2, s77
	s_mov_b32 s3, s93
	v_pk_mul_f32 v[24:25], v[18:19], s[6:7]
	v_pk_fma_f32 v[24:25], v[16:17], s[2:3], v[24:25]
	s_mov_b64 s[2:3], -1
	v_pk_mul_f32 v[8:9], v[24:25], v[8:9]
	v_add_f32_e32 v6, v8, v6
	v_add_f32_e32 v8, v9, v6
	s_nop 0
	v_lshlrev_b32_e32 v6, 16, v15
	v_mul_f32_e32 v6, v198, v6
	v_fmac_f32_e32 v6, v197, v10
	v_fmac_f32_e32 v6, v199, v7
	v_add_f32_e32 v9, v200, v6
	v_add_co_u32_e32 v6, vcc, 0x9000, v2
	s_nop 1
	v_addc_co_u32_e32 v7, vcc, 0, v3, vcc
	v_mov_b32_e32 v6, v215
	s_and_b64 vcc, exec, s[4:5]
	s_nop 0
	v_mul_f32_e32 v6, v13, v6
	v_fmac_f32_e32 v6, v201, v8
	v_mul_f32_e32 v6, v9, v6
	s_cbranch_vccnz .LBB0_784
	v_bfe_u32 v7, v6, 16, 1
	s_movk_i32 s2, 0x7fff
	v_add3_u32 v7, v6, v7, s2
	v_lshl_add_u64 v[4:5], v[4:5], 1, s[52:53]
	s_mov_b64 s[2:3], 0
	global_store_short_d16_hi v[4:5], v7, off

.LBB0_790:
	s_or_b64 exec, exec, s[2:3]
	s_mov_b32 s6, s19
	s_mov_b32 s7, s9
	s_mov_b32 s2, s9
	s_mov_b32 s3, s19
	v_pk_mul_f32 v[26:27], v[18:19], s[6:7]
	v_pk_add_f32 v[24:25], v[30:31], v[32:33] neg_lo:[0,1] neg_hi:[0,1]
	v_pk_fma_f32 v[26:27], v[16:17], s[2:3], v[26:27]
	s_mov_b64 s[2:3], -1
	v_pk_mul_f32 v[24:25], v[26:27], v[24:25]
	v_add_f32_e32 v6, v24, v6
	v_add_f32_e32 v10, v25, v6
	s_nop 0
	v_lshlrev_b32_e32 v6, 16, v9
	v_mul_f32_e32 v6, v198, v6
	v_fmac_f32_e32 v6, v197, v8
	v_fmac_f32_e32 v6, v199, v7
	v_add_f32_e32 v8, v200, v6
	v_add_co_u32_e32 v6, vcc, 0x9000, v2
	s_nop 1
	v_addc_co_u32_e32 v7, vcc, 0, v3, vcc
	v_mov_b32_e32 v6, v220
	s_and_b64 vcc, exec, s[4:5]
	s_nop 0
	v_mul_f32_e32 v6, v13, v6
	v_fmac_f32_e32 v6, v201, v10
	v_mul_f32_e32 v6, v8, v6
	s_cbranch_vccnz .LBB0_792
	v_bfe_u32 v7, v6, 16, 1
	s_movk_i32 s2, 0x7fff
	v_add3_u32 v7, v6, v7, s2
	v_lshl_add_u64 v[4:5], v[4:5], 1, s[52:53]
	s_mov_b64 s[2:3], 0
	global_store_short_d16_hi v[4:5], v7, off

.LBB0_798:
	s_or_b64 exec, exec, s[2:3]
	s_mov_b32 s6, s89
	s_mov_b32 s7, s55
	s_mov_b32 s2, s55
	s_mov_b32 s3, s89
	v_pk_mul_f32 v[26:27], v[18:19], s[6:7]
	v_pk_add_f32 v[24:25], v[34:35], v[36:37] neg_lo:[0,1] neg_hi:[0,1]
	v_pk_fma_f32 v[26:27], v[16:17], s[2:3], v[26:27]
	s_mov_b64 s[2:3], -1
	v_pk_mul_f32 v[24:25], v[26:27], v[24:25]
	v_add_f32_e32 v6, v24, v6
	v_add_f32_e32 v10, v25, v6
	s_nop 0
	v_lshlrev_b32_e32 v6, 16, v9
	v_mul_f32_e32 v6, v198, v6
	v_fmac_f32_e32 v6, v197, v8
	v_fmac_f32_e32 v6, v199, v7
	v_add_f32_e32 v8, v200, v6
	v_add_co_u32_e32 v6, vcc, 0xa000, v2
	s_nop 1
	v_addc_co_u32_e32 v7, vcc, 0, v3, vcc
	v_mov_b32_e32 v6, v225
	s_and_b64 vcc, exec, s[4:5]
	s_nop 0
	v_mul_f32_e32 v6, v13, v6
	v_fmac_f32_e32 v6, v201, v10
	v_mul_f32_e32 v6, v8, v6
	s_cbranch_vccnz .LBB0_800
	v_bfe_u32 v7, v6, 16, 1
	s_movk_i32 s2, 0x7fff
	v_add3_u32 v7, v6, v7, s2
	v_lshl_add_u64 v[4:5], v[4:5], 1, s[52:53]
	s_mov_b64 s[2:3], 0
	global_store_short_d16_hi v[4:5], v7, off

.LBB0_806:
	s_or_b64 exec, exec, s[2:3]
	s_mov_b32 s6, s17
	s_mov_b32 s7, s81
	s_mov_b32 s2, s81
	s_mov_b32 s3, s17
	v_pk_mul_f32 v[26:27], v[18:19], s[6:7]
	v_pk_add_f32 v[24:25], v[38:39], v[40:41] neg_lo:[0,1] neg_hi:[0,1]
	v_pk_fma_f32 v[26:27], v[16:17], s[2:3], v[26:27]
	s_mov_b64 s[2:3], -1
	v_pk_mul_f32 v[24:25], v[26:27], v[24:25]
	v_add_f32_e32 v6, v24, v6
	v_add_f32_e32 v10, v25, v6
	s_nop 0
	v_lshlrev_b32_e32 v6, 16, v9
	v_mul_f32_e32 v6, v198, v6
	v_fmac_f32_e32 v6, v197, v8
	v_fmac_f32_e32 v6, v199, v7
	v_add_f32_e32 v8, v200, v6
	v_add_co_u32_e32 v6, vcc, 0xa000, v2
	s_nop 1
	v_addc_co_u32_e32 v7, vcc, 0, v3, vcc
	v_mov_b32_e32 v6, v230
	s_and_b64 vcc, exec, s[4:5]
	s_nop 0
	v_mul_f32_e32 v6, v13, v6
	v_fmac_f32_e32 v6, v201, v10
	v_mul_f32_e32 v6, v8, v6
	s_cbranch_vccnz .LBB0_808
	v_bfe_u32 v7, v6, 16, 1
	s_movk_i32 s2, 0x7fff
	v_add3_u32 v7, v6, v7, s2
	v_lshl_add_u64 v[4:5], v[4:5], 1, s[52:53]
	s_mov_b64 s[2:3], 0
	global_store_short_d16_hi v[4:5], v7, off

.LBB0_814:
	s_or_b64 exec, exec, s[2:3]
	s_mov_b32 s6, s87
	s_mov_b32 s7, s11
	s_mov_b32 s2, s11
	s_mov_b32 s3, s87
	v_pk_mul_f32 v[26:27], v[18:19], s[6:7]
	v_pk_add_f32 v[24:25], v[42:43], v[44:45] neg_lo:[0,1] neg_hi:[0,1]
	v_pk_fma_f32 v[26:27], v[16:17], s[2:3], v[26:27]
	s_mov_b64 s[2:3], -1
	v_pk_mul_f32 v[24:25], v[26:27], v[24:25]
	v_add_f32_e32 v6, v24, v6
	v_add_f32_e32 v10, v25, v6
	s_nop 0
	v_lshlrev_b32_e32 v6, 16, v9
	v_mul_f32_e32 v6, v198, v6
	v_fmac_f32_e32 v6, v197, v8
	v_fmac_f32_e32 v6, v199, v7
	v_add_f32_e32 v8, v200, v6
	v_add_co_u32_e32 v6, vcc, 0xb000, v2
	s_nop 1
	v_addc_co_u32_e32 v7, vcc, 0, v3, vcc
	v_mov_b32_e32 v6, v235
	s_and_b64 vcc, exec, s[4:5]
	s_nop 0
	v_mul_f32_e32 v6, v13, v6
	v_fmac_f32_e32 v6, v201, v10
	v_mul_f32_e32 v6, v8, v6
	s_cbranch_vccnz .LBB0_816
	v_bfe_u32 v7, v6, 16, 1
	s_movk_i32 s2, 0x7fff
	v_add3_u32 v7, v6, v7, s2
	v_lshl_add_u64 v[4:5], v[4:5], 1, s[52:53]
	s_mov_b64 s[2:3], 0
	global_store_short_d16_hi v[4:5], v7, off

.LBB0_822:
	s_or_b64 exec, exec, s[2:3]
	s_mov_b32 s6, s15
	s_mov_b32 s7, s83
	s_mov_b32 s2, s83
	s_mov_b32 s3, s15
	v_pk_mul_f32 v[26:27], v[18:19], s[6:7]
	v_pk_add_f32 v[24:25], v[46:47], v[48:49] neg_lo:[0,1] neg_hi:[0,1]
	v_pk_fma_f32 v[26:27], v[16:17], s[2:3], v[26:27]
	s_mov_b64 s[2:3], -1
	v_pk_mul_f32 v[24:25], v[26:27], v[24:25]
	v_add_f32_e32 v6, v24, v6
	v_add_f32_e32 v10, v25, v6
	s_nop 0
	v_lshlrev_b32_e32 v6, 16, v9
	v_mul_f32_e32 v6, v198, v6
	v_fmac_f32_e32 v6, v197, v8
	v_fmac_f32_e32 v6, v199, v7
	v_add_f32_e32 v8, v200, v6
	v_add_co_u32_e32 v6, vcc, 0xb000, v2
	s_nop 1
	v_addc_co_u32_e32 v7, vcc, 0, v3, vcc
	v_mov_b32_e32 v6, v240
	s_and_b64 vcc, exec, s[4:5]
	s_nop 0
	v_mul_f32_e32 v6, v13, v6
	v_fmac_f32_e32 v6, v201, v10
	v_mul_f32_e32 v6, v8, v6
	s_cbranch_vccnz .LBB0_824
	v_bfe_u32 v7, v6, 16, 1
	s_movk_i32 s2, 0x7fff
	v_add3_u32 v7, v6, v7, s2
	v_lshl_add_u64 v[4:5], v[4:5], 1, s[52:53]
	s_mov_b64 s[2:3], 0
	global_store_short_d16_hi v[4:5], v7, off

.LBB0_830:
	s_or_b64 exec, exec, s[2:3]
	s_mov_b32 s2, s13
	v_pk_mul_f32 v[26:27], v[18:19], s[2:3] op_sel_hi:[1,0]
	v_pk_add_f32 v[24:25], v[50:51], v[52:53] neg_lo:[0,1] neg_hi:[0,1]
	v_pk_fma_f32 v[26:27], v[16:17], s[2:3], v[26:27] op_sel_hi:[1,0,1]
	s_mov_b64 s[2:3], -1
	v_pk_mul_f32 v[24:25], v[26:27], v[24:25]
	v_add_f32_e32 v6, v24, v6
	v_add_f32_e32 v10, v25, v6
	s_nop 0
	v_lshlrev_b32_e32 v6, 16, v9
	v_mul_f32_e32 v6, v198, v6
	v_fmac_f32_e32 v6, v197, v8
	v_fmac_f32_e32 v6, v199, v7
	v_add_f32_e32 v8, v200, v6
	v_add_co_u32_e32 v6, vcc, 0xc000, v2
	s_nop 1
	v_addc_co_u32_e32 v7, vcc, 0, v3, vcc
	v_mov_b32_e32 v6, v205
	s_and_b64 vcc, exec, s[4:5]
	s_nop 0
	v_mul_f32_e32 v6, v13, v6
	v_fmac_f32_e32 v6, v201, v10
	v_mul_f32_e32 v6, v8, v6
	s_cbranch_vccnz .LBB0_832
	v_bfe_u32 v7, v6, 16, 1
	s_movk_i32 s2, 0x7fff
	v_add3_u32 v7, v6, v7, s2
	v_lshl_add_u64 v[4:5], v[4:5], 1, s[52:53]
	s_mov_b64 s[2:3], 0
	global_store_short_d16_hi v[4:5], v7, off

.LBB0_838:
	s_or_b64 exec, exec, s[2:3]
	s_mov_b32 s6, s83
	s_mov_b32 s7, s15
	s_mov_b32 s2, s15
	s_mov_b32 s3, s83
	v_pk_mul_f32 v[26:27], v[18:19], s[6:7]
	v_pk_add_f32 v[24:25], v[54:55], v[56:57] neg_lo:[0,1] neg_hi:[0,1]
	v_pk_fma_f32 v[26:27], v[16:17], s[2:3], v[26:27]
	s_mov_b64 s[2:3], -1
	v_pk_mul_f32 v[24:25], v[26:27], v[24:25]
	v_add_f32_e32 v6, v24, v6
	v_add_f32_e32 v10, v25, v6
	s_nop 0
	v_lshlrev_b32_e32 v6, 16, v9
	v_mul_f32_e32 v6, v198, v6
	v_fmac_f32_e32 v6, v197, v8
	v_fmac_f32_e32 v6, v199, v7
	v_add_f32_e32 v8, v200, v6
	v_add_co_u32_e32 v6, vcc, 0xc000, v2
	s_nop 1
	v_addc_co_u32_e32 v7, vcc, 0, v3, vcc
	v_mov_b32_e32 v6, v210
	s_and_b64 vcc, exec, s[4:5]
	s_nop 0
	v_mul_f32_e32 v6, v13, v6
	v_fmac_f32_e32 v6, v201, v10
	v_mul_f32_e32 v6, v8, v6
	s_cbranch_vccnz .LBB0_840
	v_bfe_u32 v7, v6, 16, 1
	s_movk_i32 s2, 0x7fff
	v_add3_u32 v7, v6, v7, s2
	v_lshl_add_u64 v[4:5], v[4:5], 1, s[52:53]
	s_mov_b64 s[2:3], 0
	global_store_short_d16_hi v[4:5], v7, off

.LBB0_846:
	s_or_b64 exec, exec, s[2:3]
	s_mov_b32 s6, s11
	s_mov_b32 s7, s87
	s_mov_b32 s2, s87
	s_mov_b32 s3, s11
	v_pk_mul_f32 v[26:27], v[18:19], s[6:7]
	v_pk_add_f32 v[24:25], v[58:59], v[60:61] neg_lo:[0,1] neg_hi:[0,1]
	v_pk_fma_f32 v[26:27], v[16:17], s[2:3], v[26:27]
	s_mov_b64 s[2:3], -1
	v_pk_mul_f32 v[24:25], v[26:27], v[24:25]
	v_add_f32_e32 v6, v24, v6
	v_add_f32_e32 v10, v25, v6
	s_nop 0
	v_lshlrev_b32_e32 v6, 16, v9
	v_mul_f32_e32 v6, v198, v6
	v_fmac_f32_e32 v6, v197, v8
	v_fmac_f32_e32 v6, v199, v7
	v_add_f32_e32 v8, v200, v6
	v_add_co_u32_e32 v6, vcc, 0xd000, v2
	s_nop 1
	v_addc_co_u32_e32 v7, vcc, 0, v3, vcc
	v_mov_b32_e32 v6, v215
	s_and_b64 vcc, exec, s[4:5]
	s_nop 0
	v_mul_f32_e32 v6, v13, v6
	v_fmac_f32_e32 v6, v201, v10
	v_mul_f32_e32 v6, v8, v6
	s_cbranch_vccnz .LBB0_848
	v_bfe_u32 v7, v6, 16, 1
	s_movk_i32 s2, 0x7fff
	v_add3_u32 v7, v6, v7, s2
	v_lshl_add_u64 v[4:5], v[4:5], 1, s[52:53]
	s_mov_b64 s[2:3], 0
	global_store_short_d16_hi v[4:5], v7, off

.LBB0_854:
	s_or_b64 exec, exec, s[2:3]
	s_mov_b32 s6, s81
	s_mov_b32 s7, s17
	s_mov_b32 s2, s17
	s_mov_b32 s3, s81
	v_pk_mul_f32 v[26:27], v[18:19], s[6:7]
	v_pk_add_f32 v[24:25], v[62:63], v[64:65] neg_lo:[0,1] neg_hi:[0,1]
	v_pk_fma_f32 v[26:27], v[16:17], s[2:3], v[26:27]
	s_mov_b64 s[2:3], -1
	v_pk_mul_f32 v[24:25], v[26:27], v[24:25]
	v_add_f32_e32 v6, v24, v6
	v_add_f32_e32 v10, v25, v6
	s_nop 0
	v_lshlrev_b32_e32 v6, 16, v9
	v_mul_f32_e32 v6, v198, v6
	v_fmac_f32_e32 v6, v197, v8
	v_fmac_f32_e32 v6, v199, v7
	v_add_f32_e32 v8, v200, v6
	v_add_co_u32_e32 v6, vcc, 0xd000, v2
	s_nop 1
	v_addc_co_u32_e32 v7, vcc, 0, v3, vcc
	v_mov_b32_e32 v6, v220
	s_and_b64 vcc, exec, s[4:5]
	s_nop 0
	v_mul_f32_e32 v6, v13, v6
	v_fmac_f32_e32 v6, v201, v10
	v_mul_f32_e32 v6, v8, v6
	s_cbranch_vccnz .LBB0_856
	v_bfe_u32 v7, v6, 16, 1
	s_movk_i32 s2, 0x7fff
	v_add3_u32 v7, v6, v7, s2
	v_lshl_add_u64 v[4:5], v[4:5], 1, s[52:53]
	s_mov_b64 s[2:3], 0
	global_store_short_d16_hi v[4:5], v7, off

.LBB0_862:
	s_or_b64 exec, exec, s[2:3]
	s_mov_b32 s6, s55
	s_mov_b32 s7, s89
	s_mov_b32 s2, s89
	s_mov_b32 s3, s55
	v_pk_mul_f32 v[26:27], v[18:19], s[6:7]
	v_pk_add_f32 v[24:25], v[66:67], v[68:69] neg_lo:[0,1] neg_hi:[0,1]
	v_pk_fma_f32 v[26:27], v[16:17], s[2:3], v[26:27]
	s_mov_b64 s[2:3], -1
	v_pk_mul_f32 v[24:25], v[26:27], v[24:25]
	v_add_f32_e32 v6, v24, v6
	v_add_f32_e32 v10, v25, v6
	s_nop 0
	v_lshlrev_b32_e32 v6, 16, v9
	v_mul_f32_e32 v6, v198, v6
	v_fmac_f32_e32 v6, v197, v8
	v_fmac_f32_e32 v6, v199, v7
	v_add_f32_e32 v8, v200, v6
	v_add_co_u32_e32 v6, vcc, 0xe000, v2
	s_nop 1
	v_addc_co_u32_e32 v7, vcc, 0, v3, vcc
	v_mov_b32_e32 v6, v225
	s_and_b64 vcc, exec, s[4:5]
	s_nop 0
	v_mul_f32_e32 v6, v13, v6
	v_fmac_f32_e32 v6, v201, v10
	v_mul_f32_e32 v6, v8, v6
	s_cbranch_vccnz .LBB0_864
	v_bfe_u32 v7, v6, 16, 1
	s_movk_i32 s2, 0x7fff
	v_add3_u32 v7, v6, v7, s2
	v_lshl_add_u64 v[4:5], v[4:5], 1, s[52:53]
	s_mov_b64 s[2:3], 0
	global_store_short_d16_hi v[4:5], v7, off

.LBB0_870:
	s_or_b64 exec, exec, s[2:3]
	s_mov_b32 s6, s9
	s_mov_b32 s7, s19
	s_mov_b32 s2, s19
	s_mov_b32 s3, s9
	v_pk_mul_f32 v[26:27], v[18:19], s[6:7]
	v_pk_add_f32 v[24:25], v[70:71], v[72:73] neg_lo:[0,1] neg_hi:[0,1]
	v_pk_fma_f32 v[26:27], v[16:17], s[2:3], v[26:27]
	s_mov_b64 s[2:3], -1
	v_pk_mul_f32 v[24:25], v[26:27], v[24:25]
	v_add_f32_e32 v6, v24, v6
	v_add_f32_e32 v10, v25, v6
	s_nop 0
	v_lshlrev_b32_e32 v6, 16, v9
	v_mul_f32_e32 v6, v198, v6
	v_fmac_f32_e32 v6, v197, v8
	v_fmac_f32_e32 v6, v199, v7
	v_add_f32_e32 v8, v200, v6
	v_add_co_u32_e32 v6, vcc, 0xe000, v2
	s_nop 1
	v_addc_co_u32_e32 v7, vcc, 0, v3, vcc
	v_mov_b32_e32 v6, v230
	s_and_b64 vcc, exec, s[4:5]
	s_nop 0
	v_mul_f32_e32 v6, v13, v6
	v_fmac_f32_e32 v6, v201, v10
	v_mul_f32_e32 v6, v8, v6
	s_cbranch_vccnz .LBB0_872
	v_bfe_u32 v7, v6, 16, 1
	s_movk_i32 s2, 0x7fff
	v_add3_u32 v7, v6, v7, s2
	v_lshl_add_u64 v[4:5], v[4:5], 1, s[52:53]
	s_mov_b64 s[2:3], 0
	global_store_short_d16_hi v[4:5], v7, off

.LBB0_878:
	s_or_b64 exec, exec, s[2:3]
	s_mov_b32 s6, s77
	s_mov_b32 s7, s93
	s_mov_b32 s2, s93
	s_mov_b32 s3, s77
	v_pk_mul_f32 v[26:27], v[18:19], s[6:7]
	v_pk_add_f32 v[24:25], v[74:75], v[76:77] neg_lo:[0,1] neg_hi:[0,1]
	v_pk_fma_f32 v[26:27], v[16:17], s[2:3], v[26:27]
	s_mov_b64 s[2:3], -1
	v_pk_mul_f32 v[24:25], v[26:27], v[24:25]
	v_add_f32_e32 v6, v24, v6
	v_add_f32_e32 v10, v25, v6
	s_nop 0
	v_lshlrev_b32_e32 v6, 16, v9
	v_mul_f32_e32 v6, v198, v6
	v_fmac_f32_e32 v6, v197, v8
	v_fmac_f32_e32 v6, v199, v7
	v_add_f32_e32 v8, v200, v6
	v_add_co_u32_e32 v6, vcc, 0xf000, v2
	s_nop 1
	v_addc_co_u32_e32 v7, vcc, 0, v3, vcc
	v_mov_b32_e32 v6, v235
	s_and_b64 vcc, exec, s[4:5]
	s_nop 0
	v_mul_f32_e32 v6, v13, v6
	v_fmac_f32_e32 v6, v201, v10
	v_mul_f32_e32 v6, v8, v6
	s_cbranch_vccnz .LBB0_880
	v_bfe_u32 v7, v6, 16, 1
	s_movk_i32 s2, 0x7fff
	v_add3_u32 v7, v6, v7, s2
	v_lshl_add_u64 v[4:5], v[4:5], 1, s[52:53]
	s_mov_b64 s[2:3], 0
	global_store_short_d16_hi v[4:5], v7, off

.LBB0_886:
	s_or_b64 exec, exec, s[0:1]
	s_mov_b32 s2, s41
	s_mov_b32 s3, s31
	s_mov_b32 s0, s31
	s_mov_b32 s1, s41
	v_pk_mul_f32 v[18:19], v[18:19], s[2:3]
	v_pk_add_f32 v[14:15], v[78:79], v[80:81] neg_lo:[0,1] neg_hi:[0,1]
	v_pk_fma_f32 v[16:17], v[16:17], s[0:1], v[18:19]
	s_mov_b64 s[0:1], -1
	v_pk_mul_f32 v[14:15], v[16:17], v[14:15]
	v_add_f32_e32 v6, v14, v6
	v_add_f32_e32 v10, v15, v6
	s_nop 0
	v_lshlrev_b32_e32 v6, 16, v9
	v_mul_f32_e32 v6, v198, v6
	v_fmac_f32_e32 v6, v197, v8
	v_fmac_f32_e32 v6, v199, v7
	v_add_f32_e32 v8, v200, v6
	v_add_co_u32_e32 v6, vcc, 0xf000, v2
	s_nop 1
	v_addc_co_u32_e32 v7, vcc, 0, v3, vcc
	v_mov_b32_e32 v6, v240
	s_and_b64 vcc, exec, s[4:5]
	s_nop 0
	v_mul_f32_e32 v6, v13, v6
	v_fmac_f32_e32 v6, v201, v10
	v_mul_f32_e32 v6, v8, v6
	s_cbranch_vccnz .LBB0_888
	v_bfe_u32 v7, v6, 16, 1
	s_movk_i32 s0, 0x7fff
	v_add3_u32 v7, v6, v7, s0
	v_lshl_add_u64 v[4:5], v[4:5], 1, s[52:53]
	global_store_short_d16_hi v[4:5], v7, off
	s_cbranch_execnz .LBB0_631
	s_branch .LBB0_889

.LBB0_917:
	s_or_b64 exec, exec, s[18:19]
	v_add_f32_e32 v6, 0, v6
	v_add_f32_e32 v6, v6, v7
	v_add_f32_e32 v6, v6, v8
	v_add_f32_e32 v6, v6, v9
	v_add_f32_e32 v2, v6, v2
	v_add_f32_e32 v2, v2, v3
	v_add_f32_e32 v2, v2, v4
	v_add_f32_e32 v2, v2, v5
	v_div_scale_f32 v3, s[18:19], v2, v2, v38
	v_rcp_f32_e32 v4, v3
	s_waitcnt vmcnt(0)
	v_lshlrev_b32_e32 v27, 16, v25
	ds_read_b32 v25, v37 offset:2048
	v_fma_f32 v5, -v3, v4, 1.0
	v_fmac_f32_e32 v4, v5, v4
	v_div_scale_f32 v5, vcc, v38, v2, v38
	v_mul_f32_e32 v6, v5, v4
	v_fma_f32 v7, -v3, v6, v5
	v_fmac_f32_e32 v6, v7, v4
	v_fma_f32 v3, -v3, v6, v5
	v_div_fmas_f32 v3, v3, v4, v6
	v_div_fixup_f32 v4, v3, v2, v38
	v_mul_f32_e32 v2, v23, v27
	v_pk_fma_f32 v[2:3], v[22:23], v[26:27], v[2:3] op_sel_hi:[1,1,0]
	s_nop 0
	v_mov_b32_e32 v3, v4
	s_waitcnt lgkmcnt(0)
	v_pk_fma_f32 v[2:3], v[20:21], v[24:25], v[2:3]
	v_add_f32_e32 v2, v39, v2
	v_mul_f32_e32 v2, v2, v3

.LBB0_939:
	s_or_b64 exec, exec, s[12:13]
	v_add_f32_e32 v6, 0, v6
	v_add_f32_e32 v6, v6, v7
	v_add_f32_e32 v6, v6, v8
	v_add_f32_e32 v6, v6, v9
	v_add_f32_e32 v2, v6, v2
	v_add_f32_e32 v2, v2, v3
	v_add_f32_e32 v2, v2, v4
	v_add_f32_e32 v2, v2, v5
	v_div_scale_f32 v3, s[12:13], v2, v2, v28
	v_rcp_f32_e32 v4, v3
	s_waitcnt vmcnt(0)
	v_lshlrev_b32_e32 v27, 16, v25
	ds_read_b32 v25, v37 offset:2048
	v_fma_f32 v5, -v3, v4, 1.0
	v_fmac_f32_e32 v4, v5, v4
	v_div_scale_f32 v5, vcc, v28, v2, v28
	v_mul_f32_e32 v6, v5, v4
	v_fma_f32 v7, -v3, v6, v5
	v_fmac_f32_e32 v6, v7, v4
	v_fma_f32 v3, -v3, v6, v5
	v_div_fmas_f32 v3, v3, v4, v6
	v_div_fixup_f32 v4, v3, v2, v28
	v_mul_f32_e32 v2, v23, v27
	v_pk_fma_f32 v[2:3], v[22:23], v[26:27], v[2:3] op_sel_hi:[1,1,0]
	s_nop 0
	v_mov_b32_e32 v3, v4
	s_waitcnt lgkmcnt(0)
	v_pk_fma_f32 v[2:3], v[20:21], v[24:25], v[2:3]
	v_add_f32_e32 v2, v29, v2
	v_mul_f32_e32 v2, v2, v3

.LBB0_2730:
	s_or_b64 exec, exec, s[0:1]
	s_add_i32 s0, 0, 0x21000
	v_mov_b32_e32 v2, s0
	v_readlane_b32 s0, v251, 26
	v_mov_b32_e32 v92, v174
	s_waitcnt lgkmcnt(0)
	v_mov_b32_e32 v3, s0
	v_mov_b32_e32 v10, v164
	s_barrier
	ds_read_b128 v[6:9], v2
	ds_read_b128 v[2:5], v3
	v_mov_b32_e32 v60, v165
	v_mov_b32_e32 v34, v166
	v_mov_b32_e32 v62, v167
	v_mov_b32_e32 v32, v168
	v_mov_b32_e32 v64, v169
	v_mov_b32_e32 v38, v170
	v_mov_b32_e32 v66, v171
	v_mov_b32_e32 v10, v172
	v_pk_add_f32 v[68:69], v[14:15], v[42:43]
	v_pk_add_f32 v[14:15], v[14:15], v[42:43] neg_lo:[0,1] neg_hi:[0,1]
	v_mov_b32_e32 v13, v15
	v_mov_b32_e32 v10, v14
	v_mov_b32_e32 v42, v15
	v_mov_b32_e32 v43, v11
	v_pk_mul_f32 v[14:15], v[12:13], v[66:67] op_sel_hi:[1,0] neg_lo:[0,1] neg_hi:[0,1]
	v_pk_add_f32 v[70:71], v[18:19], v[52:53]
	v_pk_fma_f32 v[42:43], v[42:43], v[60:61], v[14:15] op_sel_hi:[1,0,1]
	v_pk_add_f32 v[14:15], v[16:17], v[48:49]
	v_pk_add_f32 v[48:49], v[16:17], v[48:49] neg_lo:[0,1] neg_hi:[0,1]
	v_mov_b32_e32 v17, v11
	v_mov_b32_e32 v13, v48
	v_mov_b32_e32 v16, v48
	v_pk_mul_f32 v[54:55], v[12:13], v[38:39] op_sel_hi:[1,0] neg_lo:[0,1] neg_hi:[0,1]
	v_mov_b32_e32 v13, v49
	v_pk_add_f32 v[18:19], v[18:19], v[52:53] neg_lo:[0,1] neg_hi:[0,1]
	v_pk_fma_f32 v[16:17], v[16:17], v[34:35], v[54:55] op_sel_hi:[1,0,1]
	v_mov_b32_e32 v54, v49
	v_mov_b32_e32 v55, v11
	v_pk_mul_f32 v[48:49], v[12:13], v[64:65] op_sel_hi:[1,0] neg_lo:[0,1] neg_hi:[0,1]
	v_mov_b32_e32 v13, v18
	v_pk_fma_f32 v[48:49], v[54:55], v[62:63], v[48:49] op_sel_hi:[1,0,1]
	v_mov_b32_e32 v52, v18
	v_mov_b32_e32 v53, v11
	v_pk_mul_f32 v[54:55], v[12:13], v[32:33] op_sel_hi:[1,0] neg_lo:[0,1] neg_hi:[0,1]
	v_mov_b32_e32 v13, v19
	v_pk_fma_f32 v[52:53], v[52:53], v[32:33], v[54:55] op_sel_hi:[1,0,1]
	v_mov_b32_e32 v54, v19
	v_mov_b32_e32 v55, v11
	v_pk_add_f32 v[18:19], v[20:21], v[50:51]
	v_pk_add_f32 v[20:21], v[20:21], v[50:51] neg_lo:[0,1] neg_hi:[0,1]
	v_pk_mul_f32 v[54:55], v[54:55], v[64:65] op_sel_hi:[1,0]
	v_mov_b32_e32 v50, v20
	v_mov_b32_e32 v51, v11
	v_pk_fma_f32 v[54:55], v[12:13], v[62:63], v[54:55] op_sel_hi:[1,0,1] neg_lo:[0,1,0] neg_hi:[0,1,0]
	v_pk_mul_f32 v[50:51], v[50:51], v[38:39] op_sel_hi:[1,0]
	v_mov_b32_e32 v13, v20
	v_pk_fma_f32 v[58:59], v[12:13], v[34:35], v[50:51] op_sel_hi:[1,0,1] neg_lo:[0,1,0] neg_hi:[0,1,0]
	v_mov_b32_e32 v50, v21
	v_mov_b32_e32 v51, v11
	v_pk_mul_f32 v[50:51], v[50:51], v[66:67] op_sel_hi:[1,0]
	v_mov_b32_e32 v13, v21
	v_pk_add_f32 v[20:21], v[24:25], v[46:47]
	v_pk_add_f32 v[24:25], v[24:25], v[46:47] neg_lo:[0,1] neg_hi:[0,1]
	v_pk_fma_f32 v[56:57], v[12:13], v[60:61], v[50:51] op_sel_hi:[1,0,1] neg_lo:[0,1,0] neg_hi:[0,1,0]
	v_xor_b32_e32 v73, 0x80000000, v24
	v_mov_b32_e32 v46, v25
	v_mov_b32_e32 v47, v11
	v_mov_b32_e32 v13, v25
	v_pk_add_f32 v[24:25], v[28:29], v[44:45]
	v_pk_add_f32 v[28:29], v[28:29], v[44:45] neg_lo:[0,1] neg_hi:[0,1]
	v_pk_mul_f32 v[46:47], v[46:47], v[66:67] op_sel_hi:[1,0] neg_lo:[0,1] neg_hi:[0,1]
	v_mov_b32_e32 v44, v28
	v_mov_b32_e32 v45, v11
	v_pk_fma_f32 v[74:75], v[12:13], v[60:61], v[46:47] op_sel_hi:[1,0,1] neg_lo:[0,1,0] neg_hi:[0,1,0]
	v_pk_mul_f32 v[44:45], v[44:45], v[38:39] op_sel_hi:[1,0] neg_lo:[0,1] neg_hi:[0,1]
	v_mov_b32_e32 v13, v28
	v_pk_fma_f32 v[76:77], v[12:13], v[34:35], v[44:45] op_sel_hi:[1,0,1] neg_lo:[0,1,0] neg_hi:[0,1,0]
	v_mov_b32_e32 v44, v29
	v_mov_b32_e32 v45, v11
	v_pk_mul_f32 v[44:45], v[44:45], v[64:65] op_sel_hi:[1,0] neg_lo:[0,1] neg_hi:[0,1]
	v_mov_b32_e32 v13, v29
	v_pk_add_f32 v[28:29], v[30:31], v[40:41]
	v_pk_add_f32 v[30:31], v[30:31], v[40:41] neg_lo:[0,1] neg_hi:[0,1]
	v_pk_fma_f32 v[78:79], v[12:13], v[62:63], v[44:45] op_sel_hi:[1,0,1] neg_lo:[0,1,0] neg_hi:[0,1,0]
	v_mov_b32_e32 v13, v30
	v_mov_b32_e32 v40, v30
	v_mov_b32_e32 v41, v11
	v_pk_mul_f32 v[44:45], v[12:13], v[32:33] op_sel_hi:[1,0] neg_lo:[0,1] neg_hi:[0,1]
	v_mov_b32_e32 v13, v31
	v_pk_fma_f32 v[80:81], v[40:41], v[32:33], v[44:45] op_sel_hi:[1,0,1] neg_lo:[0,1,0] neg_hi:[0,1,0]
	v_mov_b32_e32 v40, v31
	v_pk_mul_f32 v[30:31], v[12:13], v[64:65] op_sel_hi:[1,0] neg_lo:[0,1] neg_hi:[0,1]
	v_mov_b32_e32 v84, v11
	v_pk_fma_f32 v[62:63], v[40:41], v[62:63], v[30:31] op_sel_hi:[1,0,1] neg_lo:[0,1,0] neg_hi:[0,1,0]
	v_pk_add_f32 v[30:31], v[26:27], v[36:37]
	v_pk_add_f32 v[26:27], v[26:27], v[36:37] neg_lo:[0,1] neg_hi:[0,1]
	v_mov_b32_e32 v37, v11
	v_mov_b32_e32 v13, v26
	v_mov_b32_e32 v36, v26
	v_pk_mul_f32 v[40:41], v[12:13], v[38:39] op_sel_hi:[1,0] neg_lo:[0,1] neg_hi:[0,1]
	v_mov_b32_e32 v13, v27
	v_pk_fma_f32 v[64:65], v[36:37], v[34:35], v[40:41] op_sel_hi:[1,0,1] neg_lo:[0,1,0] neg_hi:[0,1,0]
	v_mov_b32_e32 v36, v27
	v_pk_mul_f32 v[26:27], v[12:13], v[66:67] op_sel_hi:[1,0] neg_lo:[0,1] neg_hi:[0,1]
	v_mov_b32_e32 v41, v11
	v_pk_fma_f32 v[66:67], v[36:37], v[60:61], v[26:27] op_sel_hi:[1,0,1] neg_lo:[0,1,0] neg_hi:[0,1,0]
	v_pk_add_f32 v[26:27], v[68:69], v[20:21] neg_lo:[0,1] neg_hi:[0,1]
	v_pk_add_f32 v[20:21], v[68:69], v[20:21]
	v_mov_b32_e32 v13, v27
	v_mov_b32_e32 v36, v26
	v_mov_b32_e32 v40, v27
	v_pk_mul_f32 v[26:27], v[12:13], v[38:39] op_sel_hi:[1,0] neg_lo:[0,1] neg_hi:[0,1]
	v_mov_b32_e32 v61, v11
	v_pk_fma_f32 v[44:45], v[40:41], v[34:35], v[26:27] op_sel_hi:[1,0,1]
	v_pk_add_f32 v[26:27], v[14:15], v[24:25] neg_lo:[0,1] neg_hi:[0,1]
	v_pk_add_f32 v[14:15], v[14:15], v[24:25]
	v_mov_b32_e32 v13, v26
	v_mov_b32_e32 v40, v26
	v_pk_mul_f32 v[46:47], v[12:13], v[32:33] op_sel_hi:[1,0] neg_lo:[0,1] neg_hi:[0,1]
	v_mov_b32_e32 v13, v27
	v_pk_fma_f32 v[50:51], v[40:41], v[32:33], v[46:47] op_sel_hi:[1,0,1]
	v_mov_b32_e32 v40, v27
	v_pk_mul_f32 v[40:41], v[40:41], v[38:39] op_sel_hi:[1,0]
	v_pk_add_f32 v[26:27], v[70:71], v[28:29] neg_lo:[0,1] neg_hi:[0,1]
	v_pk_fma_f32 v[82:83], v[12:13], v[34:35], v[40:41] op_sel_hi:[1,0,1] neg_lo:[0,1,0] neg_hi:[0,1,0]
	v_mov_b32_e32 v40, v27
	v_mov_b32_e32 v41, v11
	v_xor_b32_e32 v85, 0x80000000, v26
	v_pk_mul_f32 v[40:41], v[40:41], v[38:39] op_sel_hi:[1,0] neg_lo:[0,1] neg_hi:[0,1]
	v_mov_b32_e32 v13, v27
	v_pk_add_f32 v[26:27], v[18:19], v[30:31] neg_lo:[0,1] neg_hi:[0,1]
	v_pk_fma_f32 v[86:87], v[12:13], v[34:35], v[40:41] op_sel_hi:[1,0,1] neg_lo:[0,1,0] neg_hi:[0,1,0]
	v_mov_b32_e32 v13, v26
	v_mov_b32_e32 v40, v26
	v_mov_b32_e32 v41, v11
	v_pk_mul_f32 v[46:47], v[12:13], v[32:33] op_sel_hi:[1,0] neg_lo:[0,1] neg_hi:[0,1]
	v_mov_b32_e32 v13, v27
	v_pk_fma_f32 v[88:89], v[40:41], v[32:33], v[46:47] op_sel_hi:[1,0,1] neg_lo:[0,1,0] neg_hi:[0,1,0]
	v_mov_b32_e32 v40, v27
	v_pk_mul_f32 v[26:27], v[12:13], v[38:39] op_sel_hi:[1,0] neg_lo:[0,1] neg_hi:[0,1]
	v_pk_add_f32 v[24:25], v[70:71], v[28:29]
	v_pk_fma_f32 v[90:91], v[40:41], v[34:35], v[26:27] op_sel_hi:[1,0,1] neg_lo:[0,1,0] neg_hi:[0,1,0]
	v_pk_add_f32 v[26:27], v[20:21], v[24:25] neg_lo:[0,1] neg_hi:[0,1]
	v_pk_add_f32 v[18:19], v[18:19], v[30:31]
	v_mov_b32_e32 v13, v27
	v_mov_b32_e32 v28, v26
	v_pk_add_f32 v[20:21], v[20:21], v[24:25]
	v_mov_b32_e32 v24, v27
	v_mov_b32_e32 v25, v11
	v_pk_mul_f32 v[26:27], v[12:13], v[32:33] op_sel_hi:[1,0] neg_lo:[0,1] neg_hi:[0,1]
	v_mov_b32_e32 v29, v11
	v_pk_fma_f32 v[24:25], v[24:25], v[32:33], v[26:27] op_sel_hi:[1,0,1]
	v_pk_add_f32 v[26:27], v[14:15], v[18:19] neg_lo:[0,1] neg_hi:[0,1]
	v_pk_add_f32 v[14:15], v[14:15], v[18:19]
	v_mov_b32_e32 v13, v27
	v_xor_b32_e32 v41, 0x80000000, v26
	v_mov_b32_e32 v18, v27
	v_mov_b32_e32 v19, v11
	v_pk_mul_f32 v[26:27], v[12:13], v[32:33] op_sel_hi:[1,0] neg_lo:[0,1] neg_hi:[0,1]
	v_pk_add_f32 v[30:31], v[20:21], v[14:15]
	v_pk_fma_f32 v[18:19], v[18:19], v[32:33], v[26:27] op_sel_hi:[1,0,1] neg_lo:[0,1,0] neg_hi:[0,1,0]
	v_pk_add_f32 v[26:27], v[20:21], v[14:15] neg_lo:[0,1] neg_hi:[0,1]
	v_mov_b32_e32 v40, v11
	v_pk_add_f32 v[14:15], v[26:27], 0 neg_lo:[1,1] neg_hi:[1,1]
	v_mov_b32_e32 v60, v26
	v_mov_b32_e32 v14, v11
	v_pk_add_f32 v[26:27], v[24:25], v[18:19]
	v_pk_add_f32 v[18:19], v[24:25], v[18:19] neg_lo:[0,1] neg_hi:[0,1]
	v_pk_add_f32 v[46:47], v[60:61], v[14:15]
	v_pk_add_f32 v[20:21], v[60:61], v[14:15] neg_lo:[0,1] neg_hi:[0,1]
	v_pk_add_f32 v[14:15], v[28:29], v[40:41]
	v_pk_add_f32 v[28:29], v[28:29], v[40:41] neg_lo:[0,1] neg_hi:[0,1]
	v_pk_add_f32 v[60:61], v[14:15], v[26:27]
	v_pk_add_f32 v[26:27], v[14:15], v[26:27] neg_lo:[0,1] neg_hi:[0,1]
	v_pk_add_f32 v[40:41], v[28:29], v[18:19] op_sel:[0,1] op_sel_hi:[1,0] neg_hi:[0,1]
	v_pk_add_f32 v[14:15], v[28:29], v[18:19] op_sel:[0,1] op_sel_hi:[1,0] neg_lo:[0,1]
	v_pk_add_f32 v[18:19], v[36:37], v[84:85]
	v_pk_add_f32 v[28:29], v[36:37], v[84:85] neg_lo:[0,1] neg_hi:[0,1]
	v_pk_add_f32 v[36:37], v[44:45], v[86:87] neg_lo:[0,1] neg_hi:[0,1]
	v_pk_add_f32 v[24:25], v[44:45], v[86:87]
	v_pk_mul_f32 v[44:45], v[32:33], v[36:37] op_sel:[0,1] op_sel_hi:[0,0] neg_lo:[1,1] neg_hi:[1,0]
	v_pk_fma_f32 v[44:45], v[32:33], v[36:37], v[44:45] op_sel_hi:[0,1,1]
	v_pk_add_f32 v[36:37], v[50:51], v[88:89]
	v_pk_add_f32 v[50:51], v[50:51], v[88:89] neg_lo:[0,1] neg_hi:[0,1]
	v_pk_add_f32 v[70:71], v[82:83], v[90:91] neg_lo:[0,1] neg_hi:[0,1]
	v_xor_b32_e32 v69, 0x80000000, v50
	v_mov_b32_e32 v68, v51
	v_pk_add_f32 v[50:51], v[82:83], v[90:91]
	v_pk_mul_f32 v[82:83], v[32:33], v[70:71] op_sel:[0,1] op_sel_hi:[0,0] neg_lo:[1,1] neg_hi:[1,0]
	v_pk_fma_f32 v[70:71], v[32:33], v[70:71], v[82:83] op_sel_hi:[0,1,1] neg_lo:[1,0,0] neg_hi:[1,0,0]
	v_pk_add_f32 v[82:83], v[18:19], v[36:37]
	v_pk_add_f32 v[18:19], v[18:19], v[36:37] neg_lo:[0,1] neg_hi:[0,1]
	v_pk_add_f32 v[36:37], v[24:25], v[50:51]
	v_pk_add_f32 v[24:25], v[24:25], v[50:51] neg_lo:[0,1] neg_hi:[0,1]
	v_mov_b32_e32 v72, v11
	v_pk_add_f32 v[50:51], v[18:19], v[24:25] op_sel:[0,1] op_sel_hi:[1,0] neg_hi:[0,1]
	v_pk_add_f32 v[24:25], v[18:19], v[24:25] op_sel:[0,1] op_sel_hi:[1,0] neg_lo:[0,1]
	v_pk_add_f32 v[18:19], v[28:29], v[68:69]
	v_pk_add_f32 v[68:69], v[28:29], v[68:69] neg_lo:[0,1] neg_hi:[0,1]
	v_pk_add_f32 v[28:29], v[44:45], v[70:71]
	v_pk_add_f32 v[44:45], v[44:45], v[70:71] neg_lo:[0,1] neg_hi:[0,1]
	v_pk_add_f32 v[86:87], v[82:83], v[36:37]
	v_xor_b32_e32 v71, 0x80000000, v44
	v_mov_b32_e32 v70, v45
	v_pk_add_f32 v[36:37], v[82:83], v[36:37] neg_lo:[0,1] neg_hi:[0,1]
	v_pk_add_f32 v[82:83], v[18:19], v[28:29]
	v_pk_add_f32 v[28:29], v[18:19], v[28:29] neg_lo:[0,1] neg_hi:[0,1]
	v_pk_add_f32 v[44:45], v[68:69], v[70:71]
	v_pk_add_f32 v[18:19], v[68:69], v[70:71] neg_lo:[0,1] neg_hi:[0,1]
	v_pk_add_f32 v[68:69], v[10:11], v[72:73]
	v_pk_add_f32 v[70:71], v[10:11], v[72:73] neg_lo:[0,1] neg_hi:[0,1]
	v_pk_add_f32 v[72:73], v[42:43], v[74:75]
	v_pk_add_f32 v[42:43], v[42:43], v[74:75] neg_lo:[0,1] neg_hi:[0,1]
	v_add_f32_e32 v10, v30, v31
	v_pk_mul_f32 v[74:75], v[38:39], v[42:43] op_sel:[0,1] op_sel_hi:[0,0] neg_lo:[1,1] neg_hi:[1,0]
	v_pk_fma_f32 v[42:43], v[34:35], v[42:43], v[74:75] op_sel_hi:[0,1,1]
	v_pk_add_f32 v[74:75], v[16:17], v[76:77]
	v_pk_add_f32 v[16:17], v[16:17], v[76:77] neg_lo:[0,1] neg_hi:[0,1]
	v_lshl_add_u32 v13, v92, 3, 0
	v_pk_mul_f32 v[76:77], v[32:33], v[16:17] op_sel:[0,1] op_sel_hi:[0,0] neg_lo:[1,1] neg_hi:[1,0]
	v_pk_fma_f32 v[16:17], v[32:33], v[16:17], v[76:77] op_sel_hi:[0,1,1]
	v_pk_add_f32 v[76:77], v[48:49], v[78:79]
	v_pk_add_f32 v[48:49], v[48:49], v[78:79] neg_lo:[0,1] neg_hi:[0,1]
	v_pk_mul_f32 v[78:79], v[34:35], v[48:49] op_sel:[0,1] op_sel_hi:[0,0] neg_lo:[1,1] neg_hi:[1,0]
	v_pk_fma_f32 v[78:79], v[38:39], v[48:49], v[78:79] op_sel_hi:[0,1,1]
	v_pk_add_f32 v[48:49], v[52:53], v[80:81]
	v_pk_add_f32 v[52:53], v[52:53], v[80:81] neg_lo:[0,1] neg_hi:[0,1]
	v_xor_b32_e32 v81, 0x80000000, v52
	v_mov_b32_e32 v80, v53
	v_pk_add_f32 v[52:53], v[54:55], v[62:63]
	v_pk_add_f32 v[54:55], v[54:55], v[62:63] neg_lo:[0,1] neg_hi:[0,1]
	v_pk_mul_f32 v[62:63], v[34:35], v[54:55] op_sel:[0,1] op_sel_hi:[0,0] neg_lo:[1,1] neg_hi:[1,0]
	v_pk_fma_f32 v[62:63], v[38:39], v[54:55], v[62:63] op_sel_hi:[0,1,1] neg_lo:[1,0,0] neg_hi:[1,0,0]
	v_pk_add_f32 v[54:55], v[58:59], v[64:65]
	v_pk_add_f32 v[58:59], v[58:59], v[64:65] neg_lo:[0,1] neg_hi:[0,1]
	v_pk_mul_f32 v[64:65], v[32:33], v[58:59] op_sel:[0,1] op_sel_hi:[0,0] neg_lo:[1,1] neg_hi:[1,0]
	v_pk_fma_f32 v[58:59], v[32:33], v[58:59], v[64:65] op_sel_hi:[0,1,1] neg_lo:[1,0,0] neg_hi:[1,0,0]
	v_pk_add_f32 v[64:65], v[56:57], v[66:67]
	v_pk_add_f32 v[56:57], v[56:57], v[66:67] neg_lo:[0,1] neg_hi:[0,1]
	v_pk_mul_f32 v[38:39], v[38:39], v[56:57] op_sel:[0,1] op_sel_hi:[0,0] neg_lo:[1,1] neg_hi:[1,0]
	v_pk_fma_f32 v[56:57], v[34:35], v[56:57], v[38:39] op_sel_hi:[0,1,1] neg_lo:[1,0,0] neg_hi:[1,0,0]
	v_pk_add_f32 v[38:39], v[52:53], v[72:73]
	v_pk_add_f32 v[52:53], v[72:73], v[52:53] neg_lo:[0,1] neg_hi:[0,1]
	v_pk_add_f32 v[34:35], v[68:69], v[48:49]
	v_pk_mul_f32 v[66:67], v[32:33], v[52:53] op_sel:[0,1] op_sel_hi:[0,0] neg_lo:[1,1] neg_hi:[1,0]
	v_pk_fma_f32 v[52:53], v[32:33], v[52:53], v[66:67] op_sel_hi:[0,1,1]
	v_pk_add_f32 v[66:67], v[74:75], v[54:55]
	v_pk_add_f32 v[54:55], v[74:75], v[54:55] neg_lo:[0,1] neg_hi:[0,1]
	v_pk_add_f32 v[48:49], v[68:69], v[48:49] neg_lo:[0,1] neg_hi:[0,1]
	v_xor_b32_e32 v69, 0x80000000, v54
	v_mov_b32_e32 v68, v55
	v_pk_add_f32 v[54:55], v[76:77], v[64:65]
	v_pk_add_f32 v[64:65], v[76:77], v[64:65] neg_lo:[0,1] neg_hi:[0,1]
	v_pk_mul_f32 v[72:73], v[32:33], v[64:65] op_sel:[0,1] op_sel_hi:[0,0] neg_lo:[1,1] neg_hi:[1,0]
	v_pk_fma_f32 v[64:65], v[32:33], v[64:65], v[72:73] op_sel_hi:[0,1,1] neg_lo:[1,0,0] neg_hi:[1,0,0]
	v_pk_add_f32 v[72:73], v[34:35], v[66:67]
	v_pk_add_f32 v[34:35], v[34:35], v[66:67] neg_lo:[0,1] neg_hi:[0,1]
	v_pk_add_f32 v[66:67], v[38:39], v[54:55]
	v_pk_add_f32 v[38:39], v[38:39], v[54:55] neg_lo:[0,1] neg_hi:[0,1]
	v_pk_add_f32 v[76:77], v[72:73], v[66:67]
	v_pk_add_f32 v[54:55], v[72:73], v[66:67] neg_lo:[0,1] neg_hi:[0,1]
	v_pk_add_f32 v[66:67], v[34:35], v[38:39] op_sel:[0,1] op_sel_hi:[1,0] neg_hi:[0,1]
	v_pk_add_f32 v[38:39], v[34:35], v[38:39] op_sel:[0,1] op_sel_hi:[1,0] neg_lo:[0,1]
	v_pk_add_f32 v[34:35], v[48:49], v[68:69]
	v_pk_add_f32 v[68:69], v[48:49], v[68:69] neg_lo:[0,1] neg_hi:[0,1]
	v_pk_add_f32 v[48:49], v[52:53], v[64:65]
	v_pk_add_f32 v[52:53], v[52:53], v[64:65] neg_lo:[0,1] neg_hi:[0,1]
	v_pk_add_f32 v[72:73], v[34:35], v[48:49]
	v_pk_add_f32 v[48:49], v[34:35], v[48:49] neg_lo:[0,1] neg_hi:[0,1]
	v_pk_add_f32 v[74:75], v[68:69], v[52:53] op_sel:[0,1] op_sel_hi:[1,0] neg_hi:[0,1]
	v_pk_add_f32 v[34:35], v[68:69], v[52:53] op_sel:[0,1] op_sel_hi:[1,0] neg_lo:[0,1]
	v_pk_add_f32 v[68:69], v[62:63], v[42:43]
	v_pk_add_f32 v[42:43], v[42:43], v[62:63] neg_lo:[0,1] neg_hi:[0,1]
	v_pk_add_f32 v[52:53], v[70:71], v[80:81]
	v_pk_mul_f32 v[62:63], v[32:33], v[42:43] op_sel:[0,1] op_sel_hi:[0,0] neg_lo:[1,1] neg_hi:[1,0]
	v_pk_fma_f32 v[62:63], v[32:33], v[42:43], v[62:63] op_sel_hi:[0,1,1]
	v_pk_add_f32 v[42:43], v[16:17], v[58:59]
	v_pk_add_f32 v[16:17], v[16:17], v[58:59] neg_lo:[0,1] neg_hi:[0,1]
	v_pk_add_f32 v[64:65], v[70:71], v[80:81] neg_lo:[0,1] neg_hi:[0,1]
	v_xor_b32_e32 v59, 0x80000000, v16
	v_mov_b32_e32 v58, v17
	v_pk_add_f32 v[16:17], v[78:79], v[56:57]
	v_pk_add_f32 v[56:57], v[78:79], v[56:57] neg_lo:[0,1] neg_hi:[0,1]
	v_pk_mul_f32 v[70:71], v[32:33], v[56:57] op_sel:[0,1] op_sel_hi:[0,0] neg_lo:[1,1] neg_hi:[1,0]
	v_pk_fma_f32 v[32:33], v[32:33], v[56:57], v[70:71] op_sel_hi:[0,1,1] neg_lo:[1,0,0] neg_hi:[1,0,0]
	v_pk_add_f32 v[56:57], v[52:53], v[42:43]
	v_pk_add_f32 v[42:43], v[52:53], v[42:43] neg_lo:[0,1] neg_hi:[0,1]
	v_pk_add_f32 v[52:53], v[68:69], v[16:17]
	v_pk_add_f32 v[16:17], v[68:69], v[16:17] neg_lo:[0,1] neg_hi:[0,1]
	v_pk_add_f32 v[70:71], v[56:57], v[52:53]
	v_xor_b32_e32 v69, 0x80000000, v16
	v_mov_b32_e32 v68, v17
	v_pk_add_f32 v[56:57], v[56:57], v[52:53] neg_lo:[0,1] neg_hi:[0,1]
	v_pk_add_f32 v[16:17], v[64:65], v[58:59]
	v_pk_add_f32 v[52:53], v[62:63], v[32:33]
	v_pk_add_f32 v[32:33], v[62:63], v[32:33] neg_lo:[0,1] neg_hi:[0,1]
	v_pk_add_f32 v[58:59], v[64:65], v[58:59] neg_lo:[0,1] neg_hi:[0,1]
	v_pk_add_f32 v[64:65], v[16:17], v[52:53]
	v_pk_add_f32 v[52:53], v[16:17], v[52:53] neg_lo:[0,1] neg_hi:[0,1]
	v_mov_b64_e32 v[16:17], s[92:93]
	v_pk_add_f32 v[78:79], v[42:43], v[68:69]
	v_pk_add_f32 v[42:43], v[42:43], v[68:69] neg_lo:[0,1] neg_hi:[0,1]
	v_pk_add_f32 v[68:69], v[58:59], v[32:33] op_sel:[0,1] op_sel_hi:[1,0] neg_hi:[0,1]
	v_pk_add_f32 v[32:33], v[58:59], v[32:33] op_sel:[0,1] op_sel_hi:[1,0] neg_lo:[0,1]
	v_pk_fma_f32 v[58:59], v[10:11], s[42:43], v[16:17] op_sel_hi:[0,1,1]
	ds_write_b64 v13, v[58:59]
	v_pk_fma_f32 v[58:59], v[180:181], s[92:93], v[180:181] op_sel:[1,0,0] op_sel_hi:[0,1,1]
	v_pk_mul_f32 v[62:63], v[58:59], v[76:77] op_sel:[1,1] op_sel_hi:[0,1] neg_lo:[0,1]
	v_pk_fma_f32 v[62:63], v[58:59], v[76:77], v[62:63] op_sel_hi:[1,0,1]
	ds_write_b64 v13, v[62:63] offset:4224
	v_pk_mul_f32 v[62:63], v[180:181], v[58:59] op_sel:[1,1] op_sel_hi:[0,1] neg_lo:[0,1]
	v_pk_fma_f32 v[58:59], v[180:181], v[58:59], v[62:63] op_sel_hi:[1,0,1]
	v_pk_mul_f32 v[62:63], v[58:59], v[86:87] op_sel:[1,1] op_sel_hi:[0,1] neg_lo:[0,1]
	v_pk_fma_f32 v[62:63], v[58:59], v[86:87], v[62:63] op_sel_hi:[1,0,1]
	ds_write_b64 v13, v[62:63] offset:8448
	v_pk_mul_f32 v[62:63], v[180:181], v[58:59] op_sel:[1,1] op_sel_hi:[0,1] neg_lo:[0,1]
	v_pk_fma_f32 v[58:59], v[180:181], v[58:59], v[62:63] op_sel_hi:[1,0,1]
	v_pk_mul_f32 v[62:63], v[58:59], v[70:71] op_sel:[1,1] op_sel_hi:[0,1] neg_lo:[0,1]
	v_pk_fma_f32 v[62:63], v[58:59], v[70:71], v[62:63] op_sel_hi:[1,0,1]
	ds_write_b64 v13, v[62:63] offset:12672
	v_pk_mul_f32 v[62:63], v[180:181], v[58:59] op_sel:[1,1] op_sel_hi:[0,1] neg_lo:[0,1]
	v_pk_fma_f32 v[58:59], v[180:181], v[58:59], v[62:63] op_sel_hi:[1,0,1]
	v_pk_mul_f32 v[62:63], v[60:61], v[58:59] op_sel:[1,1] op_sel_hi:[1,0] neg_lo:[1,0]
	v_pk_fma_f32 v[60:61], v[60:61], v[58:59], v[62:63] op_sel_hi:[0,1,1]
	ds_write_b64 v13, v[60:61] offset:16896
	v_pk_mul_f32 v[60:61], v[180:181], v[58:59] op_sel:[1,1] op_sel_hi:[0,1] neg_lo:[0,1]
	v_pk_fma_f32 v[58:59], v[180:181], v[58:59], v[60:61] op_sel_hi:[1,0,1]
	v_pk_mul_f32 v[60:61], v[58:59], v[72:73] op_sel:[1,1] op_sel_hi:[0,1] neg_lo:[0,1]
	v_pk_fma_f32 v[60:61], v[58:59], v[72:73], v[60:61] op_sel_hi:[1,0,1]
	ds_write_b64 v13, v[60:61] offset:21120
	v_pk_mul_f32 v[60:61], v[180:181], v[58:59] op_sel:[1,1] op_sel_hi:[0,1] neg_lo:[0,1]
	v_pk_fma_f32 v[58:59], v[180:181], v[58:59], v[60:61] op_sel_hi:[1,0,1]
	v_pk_mul_f32 v[60:61], v[82:83], v[58:59] op_sel:[1,1] op_sel_hi:[1,0] neg_lo:[1,0]
	v_pk_fma_f32 v[60:61], v[82:83], v[58:59], v[60:61] op_sel_hi:[0,1,1]
	ds_write_b64 v13, v[60:61] offset:25344
	v_pk_mul_f32 v[60:61], v[180:181], v[58:59] op_sel:[1,1] op_sel_hi:[0,1] neg_lo:[0,1]
	v_pk_fma_f32 v[58:59], v[180:181], v[58:59], v[60:61] op_sel_hi:[1,0,1]
	v_pk_mul_f32 v[60:61], v[64:65], v[58:59] op_sel:[1,1] op_sel_hi:[1,0] neg_lo:[1,0]
	v_pk_fma_f32 v[60:61], v[64:65], v[58:59], v[60:61] op_sel_hi:[0,1,1]
	ds_write_b64 v13, v[60:61] offset:29568
	v_pk_mul_f32 v[60:61], v[180:181], v[58:59] op_sel:[1,1] op_sel_hi:[0,1] neg_lo:[0,1]
	v_pk_fma_f32 v[58:59], v[180:181], v[58:59], v[60:61] op_sel_hi:[1,0,1]
	v_pk_mul_f32 v[60:61], v[46:47], v[58:59] op_sel:[1,1] op_sel_hi:[1,0] neg_lo:[1,0]
	v_pk_fma_f32 v[46:47], v[46:47], v[58:59], v[60:61] op_sel_hi:[0,1,1]
	ds_write_b64 v13, v[46:47] offset:33792
	v_pk_mul_f32 v[46:47], v[180:181], v[58:59] op_sel:[1,1] op_sel_hi:[0,1] neg_lo:[0,1]
	v_pk_fma_f32 v[46:47], v[180:181], v[58:59], v[46:47] op_sel_hi:[1,0,1]
	v_pk_mul_f32 v[58:59], v[66:67], v[46:47] op_sel:[1,1] op_sel_hi:[1,0] neg_lo:[1,0]
	v_pk_fma_f32 v[58:59], v[66:67], v[46:47], v[58:59] op_sel_hi:[0,1,1]
	ds_write_b64 v13, v[58:59] offset:38016
	v_pk_mul_f32 v[58:59], v[180:181], v[46:47] op_sel:[1,1] op_sel_hi:[0,1] neg_lo:[0,1]
	v_pk_fma_f32 v[46:47], v[180:181], v[46:47], v[58:59] op_sel_hi:[1,0,1]
	v_pk_mul_f32 v[58:59], v[50:51], v[46:47] op_sel:[1,1] op_sel_hi:[1,0] neg_lo:[1,0]
	v_pk_fma_f32 v[50:51], v[50:51], v[46:47], v[58:59] op_sel_hi:[0,1,1]
	ds_write_b64 v13, v[50:51] offset:42240
	v_pk_mul_f32 v[50:51], v[180:181], v[46:47] op_sel:[1,1] op_sel_hi:[0,1] neg_lo:[0,1]
	v_pk_fma_f32 v[46:47], v[180:181], v[46:47], v[50:51] op_sel_hi:[1,0,1]
	v_pk_mul_f32 v[50:51], v[78:79], v[46:47] op_sel:[1,1] op_sel_hi:[1,0] neg_lo:[1,0]
	v_pk_fma_f32 v[50:51], v[78:79], v[46:47], v[50:51] op_sel_hi:[0,1,1]
	ds_write_b64 v13, v[50:51] offset:46464
	v_pk_mul_f32 v[50:51], v[180:181], v[46:47] op_sel:[1,1] op_sel_hi:[0,1] neg_lo:[0,1]
	v_pk_fma_f32 v[46:47], v[180:181], v[46:47], v[50:51] op_sel_hi:[1,0,1]
	v_pk_mul_f32 v[50:51], v[40:41], v[46:47] op_sel:[1,1] op_sel_hi:[1,0] neg_lo:[1,0]
	v_pk_fma_f32 v[40:41], v[40:41], v[46:47], v[50:51] op_sel_hi:[0,1,1]
	ds_write_b64 v13, v[40:41] offset:50688
	v_pk_mul_f32 v[40:41], v[180:181], v[46:47] op_sel:[1,1] op_sel_hi:[0,1] neg_lo:[0,1]
	v_pk_fma_f32 v[40:41], v[180:181], v[46:47], v[40:41] op_sel_hi:[1,0,1]
	v_pk_mul_f32 v[46:47], v[74:75], v[40:41] op_sel:[1,1] op_sel_hi:[1,0] neg_lo:[1,0]
	v_pk_fma_f32 v[46:47], v[74:75], v[40:41], v[46:47] op_sel_hi:[0,1,1]
	ds_write_b64 v13, v[46:47] offset:54912
	v_pk_mul_f32 v[46:47], v[180:181], v[40:41] op_sel:[1,1] op_sel_hi:[0,1] neg_lo:[0,1]
	v_pk_fma_f32 v[40:41], v[180:181], v[40:41], v[46:47] op_sel_hi:[1,0,1]
	v_pk_mul_f32 v[46:47], v[44:45], v[40:41] op_sel:[1,1] op_sel_hi:[1,0] neg_lo:[1,0]
	v_pk_fma_f32 v[44:45], v[44:45], v[40:41], v[46:47] op_sel_hi:[0,1,1]
	ds_write_b64 v13, v[44:45] offset:59136
	v_pk_mul_f32 v[44:45], v[180:181], v[40:41] op_sel:[1,1] op_sel_hi:[0,1] neg_lo:[0,1]
	v_pk_fma_f32 v[40:41], v[180:181], v[40:41], v[44:45] op_sel_hi:[1,0,1]
	v_pk_mul_f32 v[44:45], v[68:69], v[40:41] op_sel:[1,1] op_sel_hi:[1,0] neg_lo:[1,0]
	v_pk_fma_f32 v[44:45], v[68:69], v[40:41], v[44:45] op_sel_hi:[0,1,1]
	ds_write_b64 v13, v[44:45] offset:63360
	v_pk_mul_f32 v[44:45], v[180:181], v[40:41] op_sel:[1,1] op_sel_hi:[0,1] neg_lo:[0,1]
	v_pk_fma_f32 v[40:41], v[180:181], v[40:41], v[44:45] op_sel_hi:[1,0,1]
	s_mov_b32 s46, s43
	v_sub_f32_e32 v10, v30, v31
	v_pk_mul_f32 v[30:31], v[40:41], s[46:47]
	v_pk_fma_f32 v[30:31], v[10:11], v[40:41], v[30:31] op_sel:[0,0,1] op_sel_hi:[0,1,0]
	v_add_u32_e32 v10, 0x10800, v13
	ds_write_b64 v10, v[30:31]
	v_pk_mul_f32 v[30:31], v[180:181], v[40:41] op_sel:[1,1] op_sel_hi:[0,1] neg_lo:[0,1]
	v_pk_fma_f32 v[30:31], v[180:181], v[40:41], v[30:31] op_sel_hi:[1,0,1]
	v_pk_mul_f32 v[40:41], v[54:55], v[30:31] op_sel:[1,1] op_sel_hi:[1,0] neg_lo:[1,0]
	v_add_u32_e32 v10, 0x11880, v13
	v_pk_fma_f32 v[40:41], v[54:55], v[30:31], v[40:41] op_sel_hi:[0,1,1]
	ds_write_b64 v10, v[40:41]
	v_pk_mul_f32 v[40:41], v[180:181], v[30:31] op_sel:[1,1] op_sel_hi:[0,1] neg_lo:[0,1]
	v_pk_fma_f32 v[30:31], v[180:181], v[30:31], v[40:41] op_sel_hi:[1,0,1]
	v_pk_mul_f32 v[40:41], v[36:37], v[30:31] op_sel:[1,1] op_sel_hi:[1,0] neg_lo:[1,0]
	v_add_u32_e32 v10, 0x12900, v13
	v_pk_fma_f32 v[36:37], v[36:37], v[30:31], v[40:41] op_sel_hi:[0,1,1]
	ds_write_b64 v10, v[36:37]
	v_pk_mul_f32 v[36:37], v[180:181], v[30:31] op_sel:[1,1] op_sel_hi:[0,1] neg_lo:[0,1]
	v_pk_fma_f32 v[30:31], v[180:181], v[30:31], v[36:37] op_sel_hi:[1,0,1]
	v_pk_mul_f32 v[36:37], v[56:57], v[30:31] op_sel:[1,1] op_sel_hi:[1,0] neg_lo:[1,0]
	v_add_u32_e32 v10, 0x13980, v13
	v_pk_fma_f32 v[36:37], v[56:57], v[30:31], v[36:37] op_sel_hi:[0,1,1]
	ds_write_b64 v10, v[36:37]
	v_pk_mul_f32 v[36:37], v[180:181], v[30:31] op_sel:[1,1] op_sel_hi:[0,1] neg_lo:[0,1]
	v_pk_fma_f32 v[30:31], v[180:181], v[30:31], v[36:37] op_sel_hi:[1,0,1]
	v_pk_mul_f32 v[36:37], v[26:27], v[30:31] op_sel:[1,1] op_sel_hi:[1,0] neg_lo:[1,0]
	v_add_u32_e32 v10, 0x14a00, v13
	v_pk_fma_f32 v[26:27], v[26:27], v[30:31], v[36:37] op_sel_hi:[0,1,1]
	ds_write_b64 v10, v[26:27]
	v_pk_mul_f32 v[26:27], v[180:181], v[30:31] op_sel:[1,1] op_sel_hi:[0,1] neg_lo:[0,1]
	v_pk_fma_f32 v[26:27], v[180:181], v[30:31], v[26:27] op_sel_hi:[1,0,1]
	v_pk_mul_f32 v[30:31], v[48:49], v[26:27] op_sel:[1,1] op_sel_hi:[1,0] neg_lo:[1,0]
	v_add_u32_e32 v10, 0x15a80, v13
	v_pk_fma_f32 v[30:31], v[48:49], v[26:27], v[30:31] op_sel_hi:[0,1,1]
	ds_write_b64 v10, v[30:31]
	v_pk_mul_f32 v[30:31], v[180:181], v[26:27] op_sel:[1,1] op_sel_hi:[0,1] neg_lo:[0,1]
	v_pk_fma_f32 v[26:27], v[180:181], v[26:27], v[30:31] op_sel_hi:[1,0,1]
	v_pk_mul_f32 v[30:31], v[28:29], v[26:27] op_sel:[1,1] op_sel_hi:[1,0] neg_lo:[1,0]
	v_add_u32_e32 v10, 0x16b00, v13
	v_pk_fma_f32 v[28:29], v[28:29], v[26:27], v[30:31] op_sel_hi:[0,1,1]
	ds_write_b64 v10, v[28:29]
	v_pk_mul_f32 v[28:29], v[180:181], v[26:27] op_sel:[1,1] op_sel_hi:[0,1] neg_lo:[0,1]
	v_pk_fma_f32 v[26:27], v[180:181], v[26:27], v[28:29] op_sel_hi:[1,0,1]
	v_pk_mul_f32 v[28:29], v[52:53], v[26:27] op_sel:[1,1] op_sel_hi:[1,0] neg_lo:[1,0]
	v_add_u32_e32 v10, 0x17b80, v13
	v_pk_fma_f32 v[28:29], v[52:53], v[26:27], v[28:29] op_sel_hi:[0,1,1]
	ds_write_b64 v10, v[28:29]
	v_pk_mul_f32 v[28:29], v[180:181], v[26:27] op_sel:[1,1] op_sel_hi:[0,1] neg_lo:[0,1]
	v_pk_fma_f32 v[26:27], v[180:181], v[26:27], v[28:29] op_sel_hi:[1,0,1]
	v_pk_mul_f32 v[28:29], v[20:21], v[26:27] op_sel:[1,1] op_sel_hi:[1,0] neg_lo:[1,0]
	v_add_u32_e32 v10, 0x18c00, v13
	v_pk_fma_f32 v[20:21], v[20:21], v[26:27], v[28:29] op_sel_hi:[0,1,1]
	ds_write_b64 v10, v[20:21]
	v_pk_mul_f32 v[20:21], v[180:181], v[26:27] op_sel:[1,1] op_sel_hi:[0,1] neg_lo:[0,1]
	v_pk_fma_f32 v[20:21], v[180:181], v[26:27], v[20:21] op_sel_hi:[1,0,1]
	v_pk_mul_f32 v[26:27], v[38:39], v[20:21] op_sel:[1,1] op_sel_hi:[1,0] neg_lo:[1,0]
	v_add_u32_e32 v10, 0x19c80, v13
	v_pk_fma_f32 v[26:27], v[38:39], v[20:21], v[26:27] op_sel_hi:[0,1,1]
	ds_write_b64 v10, v[26:27]
	v_pk_mul_f32 v[26:27], v[180:181], v[20:21] op_sel:[1,1] op_sel_hi:[0,1] neg_lo:[0,1]
	v_pk_fma_f32 v[20:21], v[180:181], v[20:21], v[26:27] op_sel_hi:[1,0,1]
	v_pk_mul_f32 v[26:27], v[24:25], v[20:21] op_sel:[1,1] op_sel_hi:[1,0] neg_lo:[1,0]
	v_add_u32_e32 v10, 0x1ad00, v13
	v_pk_fma_f32 v[24:25], v[24:25], v[20:21], v[26:27] op_sel_hi:[0,1,1]
	ds_write_b64 v10, v[24:25]
	v_pk_mul_f32 v[24:25], v[180:181], v[20:21] op_sel:[1,1] op_sel_hi:[0,1] neg_lo:[0,1]
	v_pk_fma_f32 v[20:21], v[180:181], v[20:21], v[24:25] op_sel_hi:[1,0,1]
	v_pk_mul_f32 v[24:25], v[42:43], v[20:21] op_sel:[1,1] op_sel_hi:[1,0] neg_lo:[1,0]
	v_add_u32_e32 v10, 0x1bd80, v13
	v_pk_fma_f32 v[24:25], v[42:43], v[20:21], v[24:25] op_sel_hi:[0,1,1]
	ds_write_b64 v10, v[24:25]
	v_pk_mul_f32 v[24:25], v[180:181], v[20:21] op_sel:[1,1] op_sel_hi:[0,1] neg_lo:[0,1]
	v_pk_fma_f32 v[20:21], v[180:181], v[20:21], v[24:25] op_sel_hi:[1,0,1]
	v_pk_mul_f32 v[24:25], v[14:15], v[20:21] op_sel:[1,1] op_sel_hi:[1,0] neg_lo:[1,0]
	v_add_u32_e32 v10, 0x1ce00, v13
	v_pk_fma_f32 v[14:15], v[14:15], v[20:21], v[24:25] op_sel_hi:[0,1,1]
	ds_write_b64 v10, v[14:15]
	v_pk_mul_f32 v[14:15], v[180:181], v[20:21] op_sel:[1,1] op_sel_hi:[0,1] neg_lo:[0,1]
	v_pk_fma_f32 v[14:15], v[180:181], v[20:21], v[14:15] op_sel_hi:[1,0,1]
	v_pk_mul_f32 v[20:21], v[34:35], v[14:15] op_sel:[1,1] op_sel_hi:[1,0] neg_lo:[1,0]
	v_add_u32_e32 v10, 0x1de80, v13
	v_pk_fma_f32 v[20:21], v[34:35], v[14:15], v[20:21] op_sel_hi:[0,1,1]
	ds_write_b64 v10, v[20:21]
	v_pk_mul_f32 v[20:21], v[180:181], v[14:15] op_sel:[1,1] op_sel_hi:[0,1] neg_lo:[0,1]
	v_pk_fma_f32 v[14:15], v[180:181], v[14:15], v[20:21] op_sel_hi:[1,0,1]
	v_pk_mul_f32 v[20:21], v[18:19], v[14:15] op_sel:[1,1] op_sel_hi:[1,0] neg_lo:[1,0]
	v_add_u32_e32 v10, 0x1ef00, v13
	v_pk_fma_f32 v[18:19], v[18:19], v[14:15], v[20:21] op_sel_hi:[0,1,1]
	ds_write_b64 v10, v[18:19]
	v_pk_mul_f32 v[18:19], v[180:181], v[14:15] op_sel:[1,1] op_sel_hi:[0,1] neg_lo:[0,1]
	v_pk_fma_f32 v[14:15], v[180:181], v[14:15], v[18:19] op_sel_hi:[1,0,1]
	v_pk_mul_f32 v[18:19], v[32:33], v[14:15] op_sel:[1,1] op_sel_hi:[1,0] neg_lo:[1,0]
	v_add_u32_e32 v10, 0x1ff80, v13
	v_pk_fma_f32 v[14:15], v[32:33], v[14:15], v[18:19] op_sel_hi:[0,1,1]
	ds_write_b64 v10, v[14:15]
	v_mov_b32_e32 v10, v176
	v_mov_b32_e32 v13, v173
	s_waitcnt lgkmcnt(0)
	s_barrier
	v_mov_b32_e32 v14, v182
	v_xad_u32 v30, v13, 3, v10
	v_lshl_add_u32 v73, v30, 3, 0
	v_xad_u32 v30, v13, 4, v10
	v_lshl_add_u32 v72, v30, 3, 0
	v_xad_u32 v30, v13, 5, v10
	v_lshl_add_u32 v71, v30, 3, 0
	v_xad_u32 v30, v13, 6, v10
	v_lshl_add_u32 v70, v30, 3, 0
	v_xad_u32 v30, v13, 7, v10
	v_lshl_add_u32 v69, v30, 3, 0
	v_xad_u32 v30, v13, 8, v10
	v_lshl_add_u32 v30, v30, 3, 0
	v_add_u32_e32 v68, 0x800, v30
	v_xad_u32 v30, v13, 9, v10
	v_lshl_add_u32 v30, v30, 3, 0
	v_add_u32_e32 v67, 0x800, v30
	v_xad_u32 v30, v13, 10, v10
	v_lshl_add_u32 v30, v30, 3, 0
	v_add_u32_e32 v66, 0x800, v30
	v_xad_u32 v30, v13, 11, v10
	v_lshl_add_u32 v30, v30, 3, 0
	v_add_u32_e32 v18, v13, v10
	v_add_u32_e32 v65, 0x800, v30
	v_xad_u32 v30, v13, 12, v10
	v_mov_b32_e32 v15, v183
	v_lshl_add_u32 v76, v18, 3, 0
	v_lshl_add_u32 v30, v30, 3, 0
	ds_read2_b64 v[18:21], v76 offset1:16
	ds_read2_b64 v[40:43], v68 offset1:16
	v_add_u32_e32 v64, 0x800, v30
	v_xad_u32 v30, v13, 13, v10
	v_xad_u32 v22, v13, 1, v10
	v_lshl_add_u32 v30, v30, 3, 0
	v_lshl_add_u32 v75, v22, 3, 0
	v_xad_u32 v26, v13, 2, v10
	v_add_u32_e32 v63, 0x800, v30
	v_xad_u32 v30, v13, 14, v10
	v_xad_u32 v10, v13, 15, v10
	ds_read2_b64 v[22:25], v75 offset0:32 offset1:48
	ds_read2_b64 v[48:51], v67 offset0:32 offset1:48
	v_lshl_add_u32 v30, v30, 3, 0
	v_lshl_add_u32 v10, v10, 3, 0
	v_lshl_add_u32 v74, v26, 3, 0
	v_add_u32_e32 v62, 0x800, v30
	v_add_u32_e32 v13, 0x800, v10
	v_mov_b32_e32 v10, v164
	ds_read2_b64 v[26:29], v74 offset0:64 offset1:80
	ds_read2_b64 v[58:61], v73 offset0:96 offset1:112
	ds_read2_b64 v[78:81], v72 offset0:128 offset1:144
	ds_read2_b64 v[82:85], v71 offset0:160 offset1:176
	ds_read2_b64 v[86:89], v70 offset0:192 offset1:208
	ds_read2_b64 v[90:93], v69 offset0:224 offset1:240
	ds_read2_b64 v[54:57], v66 offset0:64 offset1:80
	ds_read2_b64 v[94:97], v65 offset0:96 offset1:112
	ds_read2_b64 v[98:101], v64 offset0:128 offset1:144
	ds_read2_b64 v[102:105], v63 offset0:160 offset1:176
	ds_read2_b64 v[106:109], v62 offset0:192 offset1:208
	ds_read2_b64 v[110:113], v13 offset0:224 offset1:240
	s_waitcnt lgkmcnt(14)
	v_pk_add_f32 v[114:115], v[18:19], v[40:41]
	v_pk_add_f32 v[40:41], v[18:19], v[40:41] neg_lo:[0,1] neg_hi:[0,1]
	v_pk_add_f32 v[18:19], v[20:21], v[42:43]
	v_pk_add_f32 v[20:21], v[20:21], v[42:43] neg_lo:[0,1] neg_hi:[0,1]
	v_mov_b32_e32 v30, v165
	v_mov_b32_e32 v32, v166
	v_mov_b32_e32 v34, v167
	v_mov_b32_e32 v10, v168
	v_mov_b32_e32 v38, v169
	v_mov_b32_e32 v36, v170
	v_mov_b32_e32 v46, v171
	v_mov_b32_e32 v31, v172
	v_pk_mul_f32 v[42:43], v[20:21], v[46:47] op_sel:[1,0] op_sel_hi:[0,0] neg_lo:[1,1] neg_hi:[0,1]
	s_mov_b32 s14, s43
	v_pk_fma_f32 v[44:45], v[20:21], v[30:31], v[42:43] op_sel_hi:[1,0,1]
	s_waitcnt lgkmcnt(12)
	v_pk_add_f32 v[20:21], v[22:23], v[48:49]
	v_pk_add_f32 v[22:23], v[22:23], v[48:49] neg_lo:[0,1] neg_hi:[0,1]
	s_mov_b32 s15, s42
	v_pk_mul_f32 v[42:43], v[22:23], v[36:37] op_sel:[1,0] op_sel_hi:[0,0] neg_lo:[1,1] neg_hi:[0,1]
	v_pk_fma_f32 v[48:49], v[22:23], v[32:33], v[42:43] op_sel_hi:[1,0,1]
	v_pk_add_f32 v[22:23], v[24:25], v[50:51]
	v_pk_add_f32 v[24:25], v[24:25], v[50:51] neg_lo:[0,1] neg_hi:[0,1]
	v_pk_mul_f32 v[42:43], v[24:25], v[38:39] op_sel:[1,0] op_sel_hi:[0,0] neg_lo:[1,1] neg_hi:[0,1]
	v_pk_fma_f32 v[52:53], v[24:25], v[34:35], v[42:43] op_sel_hi:[1,0,1]
	s_waitcnt lgkmcnt(5)
	v_pk_add_f32 v[24:25], v[26:27], v[54:55]
	v_pk_add_f32 v[26:27], v[26:27], v[54:55] neg_lo:[0,1] neg_hi:[0,1]
	v_pk_mul_f32 v[42:43], v[26:27], v[10:11] op_sel:[1,0] op_sel_hi:[0,0] neg_lo:[1,1] neg_hi:[0,1]
	v_pk_fma_f32 v[54:55], v[26:27], v[10:11], v[42:43] op_sel_hi:[1,0,1]
	v_pk_add_f32 v[26:27], v[28:29], v[56:57]
	v_pk_add_f32 v[28:29], v[28:29], v[56:57] neg_lo:[0,1] neg_hi:[0,1]
	v_pk_mul_f32 v[42:43], v[28:29], v[38:39] op_sel_hi:[1,0]
	v_pk_fma_f32 v[56:57], v[28:29], v[34:35], v[42:43] op_sel:[1,0,0] op_sel_hi:[0,0,1] neg_lo:[1,1,0] neg_hi:[0,1,0]
	s_waitcnt lgkmcnt(4)
	v_pk_add_f32 v[42:43], v[58:59], v[94:95] neg_lo:[0,1] neg_hi:[0,1]
	v_pk_add_f32 v[28:29], v[58:59], v[94:95]
	v_pk_mul_f32 v[50:51], v[42:43], v[36:37] op_sel_hi:[1,0]
	v_pk_fma_f32 v[58:59], v[42:43], v[32:33], v[50:51] op_sel:[1,0,0] op_sel_hi:[0,0,1] neg_lo:[1,1,0] neg_hi:[0,1,0]
	v_pk_add_f32 v[50:51], v[60:61], v[96:97] neg_lo:[0,1] neg_hi:[0,1]
	v_pk_add_f32 v[42:43], v[60:61], v[96:97]
	v_pk_mul_f32 v[60:61], v[50:51], v[46:47] op_sel_hi:[1,0]
	v_xor_b32_e32 v94, 0x80000000, v51
	v_mov_b32_e32 v95, v50
	s_waitcnt lgkmcnt(3)
	v_pk_add_f32 v[50:51], v[78:79], v[98:99]
	v_pk_add_f32 v[78:79], v[78:79], v[98:99] neg_lo:[0,1] neg_hi:[0,1]
	v_pk_fma_f32 v[60:61], v[94:95], v[30:31], v[60:61] op_sel_hi:[1,0,1] neg_lo:[0,1,0] neg_hi:[0,1,0]
	v_xor_b32_e32 v95, 0x80000000, v78
	v_mov_b32_e32 v94, v79
	v_pk_add_f32 v[78:79], v[80:81], v[100:101]
	v_pk_add_f32 v[80:81], v[80:81], v[100:101] neg_lo:[0,1] neg_hi:[0,1]
	v_pk_mul_f32 v[96:97], v[80:81], v[46:47] op_sel_hi:[1,0] neg_lo:[0,1] neg_hi:[0,1]
	v_pk_fma_f32 v[80:81], v[80:81], v[30:31], v[96:97] op_sel:[1,0,0] op_sel_hi:[0,0,1] neg_lo:[1,1,0] neg_hi:[0,1,0]
	s_waitcnt lgkmcnt(2)
	v_pk_add_f32 v[96:97], v[82:83], v[102:103]
	v_pk_add_f32 v[82:83], v[82:83], v[102:103] neg_lo:[0,1] neg_hi:[0,1]
	v_pk_mul_f32 v[98:99], v[82:83], v[36:37] op_sel_hi:[1,0] neg_lo:[0,1] neg_hi:[0,1]
	v_pk_fma_f32 v[82:83], v[82:83], v[32:33], v[98:99] op_sel:[1,0,0] op_sel_hi:[0,0,1] neg_lo:[1,1,0] neg_hi:[0,1,0]
	v_pk_add_f32 v[98:99], v[84:85], v[104:105]
	v_pk_add_f32 v[84:85], v[84:85], v[104:105] neg_lo:[0,1] neg_hi:[0,1]
	v_pk_mul_f32 v[100:101], v[84:85], v[38:39] op_sel_hi:[1,0] neg_lo:[0,1] neg_hi:[0,1]
	v_pk_fma_f32 v[84:85], v[84:85], v[34:35], v[100:101] op_sel:[1,0,0] op_sel_hi:[0,0,1] neg_lo:[1,1,0] neg_hi:[0,1,0]
	s_waitcnt lgkmcnt(1)
	v_pk_add_f32 v[100:101], v[86:87], v[106:107]
	v_pk_add_f32 v[86:87], v[86:87], v[106:107] neg_lo:[0,1] neg_hi:[0,1]
	v_pk_mul_f32 v[102:103], v[86:87], v[10:11] op_sel:[1,0] op_sel_hi:[0,0] neg_lo:[1,1] neg_hi:[0,1]
	v_pk_fma_f32 v[86:87], v[86:87], v[10:11], v[102:103] op_sel_hi:[1,0,1] neg_lo:[0,1,0] neg_hi:[0,1,0]
	v_pk_add_f32 v[102:103], v[88:89], v[108:109]
	v_pk_add_f32 v[88:89], v[88:89], v[108:109] neg_lo:[0,1] neg_hi:[0,1]
	v_pk_mul_f32 v[38:39], v[88:89], v[38:39] op_sel:[1,0] op_sel_hi:[0,0] neg_lo:[1,1] neg_hi:[0,1]
	v_pk_fma_f32 v[88:89], v[88:89], v[34:35], v[38:39] op_sel_hi:[1,0,1] neg_lo:[0,1,0] neg_hi:[0,1,0]
	s_waitcnt lgkmcnt(0)
	v_pk_add_f32 v[38:39], v[90:91], v[110:111] neg_lo:[0,1] neg_hi:[0,1]
	v_pk_add_f32 v[34:35], v[90:91], v[110:111]
	v_pk_mul_f32 v[90:91], v[38:39], v[36:37] op_sel:[1,0] op_sel_hi:[0,0] neg_lo:[1,1] neg_hi:[0,1]
	v_pk_fma_f32 v[90:91], v[38:39], v[32:33], v[90:91] op_sel_hi:[1,0,1] neg_lo:[0,1,0] neg_hi:[0,1,0]
	v_pk_add_f32 v[38:39], v[92:93], v[112:113]
	v_pk_add_f32 v[92:93], v[92:93], v[112:113] neg_lo:[0,1] neg_hi:[0,1]
	v_pk_mul_f32 v[46:47], v[92:93], v[46:47] op_sel:[1,0] op_sel_hi:[0,0] neg_lo:[1,1] neg_hi:[0,1]
	v_pk_fma_f32 v[92:93], v[92:93], v[30:31], v[46:47] op_sel_hi:[1,0,1] neg_lo:[0,1,0] neg_hi:[0,1,0]
	v_pk_add_f32 v[46:47], v[18:19], v[78:79]
	v_pk_add_f32 v[18:19], v[18:19], v[78:79] neg_lo:[0,1] neg_hi:[0,1]
	v_pk_add_f32 v[30:31], v[114:115], v[50:51]
	v_pk_mul_f32 v[78:79], v[18:19], v[36:37] op_sel:[1,0] op_sel_hi:[0,0] neg_lo:[1,1] neg_hi:[0,1]
	v_pk_add_f32 v[50:51], v[114:115], v[50:51] neg_lo:[0,1] neg_hi:[0,1]
	v_pk_fma_f32 v[78:79], v[18:19], v[32:33], v[78:79] op_sel_hi:[1,0,1]
	v_pk_add_f32 v[18:19], v[20:21], v[96:97]
	v_pk_add_f32 v[20:21], v[20:21], v[96:97] neg_lo:[0,1] neg_hi:[0,1]
	v_pk_mul_f32 v[96:97], v[20:21], v[10:11] op_sel:[1,0] op_sel_hi:[0,0] neg_lo:[1,1] neg_hi:[0,1]
	v_pk_fma_f32 v[20:21], v[20:21], v[10:11], v[96:97] op_sel_hi:[1,0,1]
	v_pk_add_f32 v[96:97], v[22:23], v[98:99]
	v_pk_add_f32 v[22:23], v[22:23], v[98:99] neg_lo:[0,1] neg_hi:[0,1]
	v_pk_mul_f32 v[98:99], v[22:23], v[36:37] op_sel_hi:[1,0]
	v_xor_b32_e32 v104, 0x80000000, v23
	v_mov_b32_e32 v105, v22
	v_pk_add_f32 v[22:23], v[24:25], v[100:101]
	v_pk_add_f32 v[24:25], v[24:25], v[100:101] neg_lo:[0,1] neg_hi:[0,1]
	v_pk_fma_f32 v[98:99], v[104:105], v[32:33], v[98:99] op_sel_hi:[1,0,1] neg_lo:[0,1,0] neg_hi:[0,1,0]
	v_xor_b32_e32 v101, 0x80000000, v24
	v_mov_b32_e32 v100, v25
	v_pk_add_f32 v[24:25], v[26:27], v[102:103]
	v_pk_add_f32 v[26:27], v[26:27], v[102:103] neg_lo:[0,1] neg_hi:[0,1]
	v_pk_mul_f32 v[102:103], v[26:27], v[36:37] op_sel_hi:[1,0] neg_lo:[0,1] neg_hi:[0,1]
	v_xor_b32_e32 v104, 0x80000000, v27
	v_mov_b32_e32 v105, v26
	v_pk_add_f32 v[26:27], v[28:29], v[34:35]
	v_pk_add_f32 v[28:29], v[28:29], v[34:35] neg_lo:[0,1] neg_hi:[0,1]
	v_pk_fma_f32 v[102:103], v[104:105], v[32:33], v[102:103] op_sel_hi:[1,0,1] neg_lo:[0,1,0] neg_hi:[0,1,0]
	v_pk_mul_f32 v[34:35], v[28:29], v[10:11] op_sel:[1,0] op_sel_hi:[0,0] neg_lo:[1,1] neg_hi:[0,1]
	v_pk_add_f32 v[104:105], v[30:31], v[22:23] neg_lo:[0,1] neg_hi:[0,1]
	v_pk_fma_f32 v[28:29], v[28:29], v[10:11], v[34:35] op_sel_hi:[1,0,1] neg_lo:[0,1,0] neg_hi:[0,1,0]
	v_pk_add_f32 v[34:35], v[42:43], v[38:39]
	v_pk_add_f32 v[38:39], v[42:43], v[38:39] neg_lo:[0,1] neg_hi:[0,1]
	v_pk_mul_f32 v[42:43], v[38:39], v[36:37] op_sel:[1,0] op_sel_hi:[0,0] neg_lo:[1,1] neg_hi:[0,1]
	v_pk_fma_f32 v[42:43], v[38:39], v[32:33], v[42:43] op_sel_hi:[1,0,1] neg_lo:[0,1,0] neg_hi:[0,1,0]
	v_pk_add_f32 v[38:39], v[30:31], v[22:23]
	v_pk_add_f32 v[22:23], v[46:47], v[24:25]
	v_pk_add_f32 v[24:25], v[46:47], v[24:25] neg_lo:[0,1] neg_hi:[0,1]
	v_pk_mul_f32 v[30:31], v[24:25], v[10:11] op_sel:[1,0] op_sel_hi:[0,0] neg_lo:[1,1] neg_hi:[0,1]
	v_pk_fma_f32 v[24:25], v[24:25], v[10:11], v[30:31] op_sel_hi:[1,0,1]
	v_pk_add_f32 v[30:31], v[18:19], v[26:27]
	v_pk_add_f32 v[18:19], v[18:19], v[26:27] neg_lo:[0,1] neg_hi:[0,1]
	v_xor_b32_e32 v27, 0x80000000, v18
	v_mov_b32_e32 v26, v19
	v_pk_add_f32 v[18:19], v[96:97], v[34:35]
	v_pk_add_f32 v[34:35], v[96:97], v[34:35] neg_lo:[0,1] neg_hi:[0,1]
	v_pk_mul_f32 v[46:47], v[34:35], v[10:11] op_sel:[1,0] op_sel_hi:[0,0] neg_lo:[1,1] neg_hi:[0,1]
	v_pk_fma_f32 v[34:35], v[34:35], v[10:11], v[46:47] op_sel_hi:[1,0,1] neg_lo:[0,1,0] neg_hi:[0,1,0]
	v_pk_add_f32 v[46:47], v[38:39], v[30:31]
	v_pk_add_f32 v[38:39], v[38:39], v[30:31] neg_lo:[0,1] neg_hi:[0,1]
	v_pk_add_f32 v[30:31], v[22:23], v[18:19]
	v_pk_add_f32 v[18:19], v[22:23], v[18:19] neg_lo:[0,1] neg_hi:[0,1]
	v_pk_add_f32 v[96:97], v[46:47], v[30:31]
	v_xor_b32_e32 v23, 0x80000000, v18
	v_mov_b32_e32 v22, v19
	v_pk_add_f32 v[18:19], v[104:105], v[26:27]
	v_pk_add_f32 v[104:105], v[104:105], v[26:27] neg_lo:[0,1] neg_hi:[0,1]
	v_pk_add_f32 v[26:27], v[24:25], v[34:35]
	v_pk_add_f32 v[24:25], v[24:25], v[34:35] neg_lo:[0,1] neg_hi:[0,1]
	v_pk_add_f32 v[30:31], v[46:47], v[30:31] neg_lo:[0,1] neg_hi:[0,1]
	v_xor_b32_e32 v35, 0x80000000, v24
	v_mov_b32_e32 v34, v25
	v_pk_add_f32 v[24:25], v[50:51], v[100:101]
	v_pk_add_f32 v[100:101], v[50:51], v[100:101] neg_lo:[0,1] neg_hi:[0,1]
	v_pk_add_f32 v[50:51], v[78:79], v[102:103] neg_lo:[0,1] neg_hi:[0,1]
	v_pk_add_f32 v[46:47], v[38:39], v[22:23]
	v_pk_add_f32 v[22:23], v[38:39], v[22:23] neg_lo:[0,1] neg_hi:[0,1]
	v_pk_add_f32 v[106:107], v[18:19], v[26:27]
	v_pk_add_f32 v[26:27], v[18:19], v[26:27] neg_lo:[0,1] neg_hi:[0,1]
	v_pk_add_f32 v[38:39], v[104:105], v[34:35]
	v_pk_add_f32 v[18:19], v[104:105], v[34:35] neg_lo:[0,1] neg_hi:[0,1]
	v_pk_add_f32 v[34:35], v[78:79], v[102:103]
	v_pk_mul_f32 v[78:79], v[10:11], v[50:51] op_sel:[0,1] op_sel_hi:[0,0] neg_lo:[1,1] neg_hi:[1,0]
	v_pk_fma_f32 v[78:79], v[10:11], v[50:51], v[78:79] op_sel_hi:[0,1,1]
	v_pk_add_f32 v[50:51], v[20:21], v[28:29]
	v_pk_add_f32 v[20:21], v[20:21], v[28:29] neg_lo:[0,1] neg_hi:[0,1]
	v_xor_b32_e32 v29, 0x80000000, v20
	v_mov_b32_e32 v28, v21
	v_pk_add_f32 v[20:21], v[98:99], v[42:43]
	v_pk_add_f32 v[42:43], v[98:99], v[42:43] neg_lo:[0,1] neg_hi:[0,1]
	v_pk_mul_f32 v[98:99], v[10:11], v[42:43] op_sel:[0,1] op_sel_hi:[0,0] neg_lo:[1,1] neg_hi:[1,0]
	v_pk_fma_f32 v[42:43], v[10:11], v[42:43], v[98:99] op_sel_hi:[0,1,1] neg_lo:[1,0,0] neg_hi:[1,0,0]
	v_pk_add_f32 v[98:99], v[24:25], v[50:51]
	v_pk_add_f32 v[24:25], v[24:25], v[50:51] neg_lo:[0,1] neg_hi:[0,1]
	v_pk_add_f32 v[50:51], v[34:35], v[20:21]
	v_pk_add_f32 v[20:21], v[34:35], v[20:21] neg_lo:[0,1] neg_hi:[0,1]
	v_pk_add_f32 v[104:105], v[98:99], v[50:51]
	v_xor_b32_e32 v103, 0x80000000, v20
	v_mov_b32_e32 v102, v21
	v_pk_add_f32 v[34:35], v[98:99], v[50:51] neg_lo:[0,1] neg_hi:[0,1]
	v_pk_add_f32 v[20:21], v[100:101], v[28:29]
	v_pk_add_f32 v[98:99], v[100:101], v[28:29] neg_lo:[0,1] neg_hi:[0,1]
	v_pk_add_f32 v[28:29], v[78:79], v[42:43]
	v_pk_add_f32 v[42:43], v[78:79], v[42:43] neg_lo:[0,1] neg_hi:[0,1]
	v_pk_add_f32 v[100:101], v[20:21], v[28:29]
	v_xor_b32_e32 v79, 0x80000000, v42
	v_mov_b32_e32 v78, v43
	v_pk_add_f32 v[28:29], v[20:21], v[28:29] neg_lo:[0,1] neg_hi:[0,1]
	v_pk_add_f32 v[42:43], v[98:99], v[78:79]
	v_pk_add_f32 v[20:21], v[98:99], v[78:79] neg_lo:[0,1] neg_hi:[0,1]
	v_pk_add_f32 v[78:79], v[40:41], v[94:95]
	v_pk_add_f32 v[94:95], v[40:41], v[94:95] neg_lo:[0,1] neg_hi:[0,1]
	v_pk_add_f32 v[40:41], v[44:45], v[80:81]
	v_pk_add_f32 v[44:45], v[44:45], v[80:81] neg_lo:[0,1] neg_hi:[0,1]
	v_pk_add_f32 v[50:51], v[24:25], v[102:103]
	v_pk_mul_f32 v[80:81], v[36:37], v[44:45] op_sel:[0,1] op_sel_hi:[0,0] neg_lo:[1,1] neg_hi:[1,0]
	v_pk_fma_f32 v[44:45], v[32:33], v[44:45], v[80:81] op_sel_hi:[0,1,1]
	v_pk_add_f32 v[80:81], v[48:49], v[82:83]
	v_pk_add_f32 v[48:49], v[48:49], v[82:83] neg_lo:[0,1] neg_hi:[0,1]
	v_pk_add_f32 v[24:25], v[24:25], v[102:103] neg_lo:[0,1] neg_hi:[0,1]
	v_pk_mul_f32 v[82:83], v[10:11], v[48:49] op_sel:[0,1] op_sel_hi:[0,0] neg_lo:[1,1] neg_hi:[1,0]
	v_pk_fma_f32 v[82:83], v[10:11], v[48:49], v[82:83] op_sel_hi:[0,1,1]
	v_pk_add_f32 v[48:49], v[52:53], v[84:85]
	v_pk_add_f32 v[52:53], v[52:53], v[84:85] neg_lo:[0,1] neg_hi:[0,1]
	v_pk_mul_f32 v[84:85], v[32:33], v[52:53] op_sel:[0,1] op_sel_hi:[0,0] neg_lo:[1,1] neg_hi:[1,0]
	v_pk_fma_f32 v[52:53], v[36:37], v[52:53], v[84:85] op_sel_hi:[0,1,1]
	v_pk_add_f32 v[84:85], v[54:55], v[86:87]
	v_pk_add_f32 v[54:55], v[54:55], v[86:87] neg_lo:[0,1] neg_hi:[0,1]
	v_xor_b32_e32 v87, 0x80000000, v54
	v_mov_b32_e32 v86, v55
	v_pk_add_f32 v[54:55], v[56:57], v[88:89]
	v_pk_add_f32 v[56:57], v[56:57], v[88:89] neg_lo:[0,1] neg_hi:[0,1]
	v_pk_mul_f32 v[88:89], v[32:33], v[56:57] op_sel:[0,1] op_sel_hi:[0,0] neg_lo:[1,1] neg_hi:[1,0]
	v_pk_fma_f32 v[56:57], v[36:37], v[56:57], v[88:89] op_sel_hi:[0,1,1] neg_lo:[1,0,0] neg_hi:[1,0,0]
	v_pk_add_f32 v[88:89], v[58:59], v[90:91]
	v_pk_add_f32 v[58:59], v[58:59], v[90:91] neg_lo:[0,1] neg_hi:[0,1]
	v_pk_mul_f32 v[90:91], v[10:11], v[58:59] op_sel:[0,1] op_sel_hi:[0,0] neg_lo:[1,1] neg_hi:[1,0]
	v_pk_fma_f32 v[58:59], v[10:11], v[58:59], v[90:91] op_sel_hi:[0,1,1] neg_lo:[1,0,0] neg_hi:[1,0,0]
	v_pk_add_f32 v[90:91], v[60:61], v[92:93]
	v_pk_add_f32 v[60:61], v[60:61], v[92:93] neg_lo:[0,1] neg_hi:[0,1]
	v_pk_mul_f32 v[36:37], v[36:37], v[60:61] op_sel:[0,1] op_sel_hi:[0,0] neg_lo:[1,1] neg_hi:[1,0]
	v_pk_fma_f32 v[36:37], v[32:33], v[60:61], v[36:37] op_sel_hi:[0,1,1] neg_lo:[1,0,0] neg_hi:[1,0,0]
	v_pk_add_f32 v[32:33], v[78:79], v[84:85]
	v_pk_add_f32 v[60:61], v[78:79], v[84:85] neg_lo:[0,1] neg_hi:[0,1]
	v_pk_add_f32 v[78:79], v[54:55], v[40:41]
	v_pk_add_f32 v[40:41], v[40:41], v[54:55] neg_lo:[0,1] neg_hi:[0,1]
	v_pk_mul_f32 v[54:55], v[10:11], v[40:41] op_sel:[0,1] op_sel_hi:[0,0] neg_lo:[1,1] neg_hi:[1,0]
	v_pk_fma_f32 v[54:55], v[10:11], v[40:41], v[54:55] op_sel_hi:[0,1,1]
	v_pk_add_f32 v[40:41], v[80:81], v[88:89]
	v_pk_add_f32 v[80:81], v[80:81], v[88:89] neg_lo:[0,1] neg_hi:[0,1]
	v_xor_b32_e32 v85, 0x80000000, v80
	v_mov_b32_e32 v84, v81
	v_pk_add_f32 v[80:81], v[48:49], v[90:91]
	v_pk_add_f32 v[48:49], v[48:49], v[90:91] neg_lo:[0,1] neg_hi:[0,1]
	v_pk_add_f32 v[90:91], v[78:79], v[80:81]
	v_pk_mul_f32 v[88:89], v[10:11], v[48:49] op_sel:[0,1] op_sel_hi:[0,0] neg_lo:[1,1] neg_hi:[1,0]
	v_pk_fma_f32 v[48:49], v[10:11], v[48:49], v[88:89] op_sel_hi:[0,1,1] neg_lo:[1,0,0] neg_hi:[1,0,0]
	v_pk_add_f32 v[88:89], v[32:33], v[40:41]
	v_pk_add_f32 v[32:33], v[32:33], v[40:41] neg_lo:[0,1] neg_hi:[0,1]
	v_pk_add_f32 v[40:41], v[78:79], v[80:81] neg_lo:[0,1] neg_hi:[0,1]
	v_pk_add_f32 v[80:81], v[88:89], v[90:91] neg_lo:[0,1] neg_hi:[0,1]
	v_pk_add_f32 v[92:93], v[32:33], v[40:41] op_sel:[0,1] op_sel_hi:[1,0] neg_hi:[0,1]
	v_pk_add_f32 v[40:41], v[32:33], v[40:41] op_sel:[0,1] op_sel_hi:[1,0] neg_lo:[0,1]
	v_pk_add_f32 v[78:79], v[54:55], v[48:49]
	v_pk_add_f32 v[48:49], v[54:55], v[48:49] neg_lo:[0,1] neg_hi:[0,1]
	v_pk_add_f32 v[32:33], v[60:61], v[84:85]
	v_pk_add_f32 v[60:61], v[60:61], v[84:85] neg_lo:[0,1] neg_hi:[0,1]
	v_xor_b32_e32 v55, 0x80000000, v48
	v_mov_b32_e32 v54, v49
	v_pk_add_f32 v[84:85], v[32:33], v[78:79]
	v_pk_add_f32 v[48:49], v[32:33], v[78:79] neg_lo:[0,1] neg_hi:[0,1]
	v_pk_add_f32 v[78:79], v[60:61], v[54:55]
	v_pk_add_f32 v[32:33], v[60:61], v[54:55] neg_lo:[0,1] neg_hi:[0,1]
	v_pk_add_f32 v[54:55], v[94:95], v[86:87]
	v_pk_add_f32 v[60:61], v[94:95], v[86:87] neg_lo:[0,1] neg_hi:[0,1]
	v_pk_add_f32 v[86:87], v[56:57], v[44:45]
	v_pk_add_f32 v[44:45], v[44:45], v[56:57] neg_lo:[0,1] neg_hi:[0,1]
	v_pk_add_f32 v[88:89], v[88:89], v[90:91]
	v_pk_mul_f32 v[56:57], v[10:11], v[44:45] op_sel:[0,1] op_sel_hi:[0,0] neg_lo:[1,1] neg_hi:[1,0]
	v_pk_fma_f32 v[56:57], v[10:11], v[44:45], v[56:57] op_sel_hi:[0,1,1]
	v_pk_add_f32 v[44:45], v[82:83], v[58:59]
	v_pk_add_f32 v[58:59], v[82:83], v[58:59] neg_lo:[0,1] neg_hi:[0,1]
	v_xor_b32_e32 v83, 0x80000000, v58
	v_mov_b32_e32 v82, v59
	v_pk_add_f32 v[58:59], v[52:53], v[36:37]
	v_pk_add_f32 v[36:37], v[52:53], v[36:37] neg_lo:[0,1] neg_hi:[0,1]
	v_pk_mul_f32 v[52:53], v[10:11], v[36:37] op_sel:[0,1] op_sel_hi:[0,0] neg_lo:[1,1] neg_hi:[1,0]
	v_pk_fma_f32 v[36:37], v[10:11], v[36:37], v[52:53] op_sel_hi:[0,1,1] neg_lo:[1,0,0] neg_hi:[1,0,0]
	v_pk_add_f32 v[52:53], v[54:55], v[44:45]
	v_pk_add_f32 v[44:45], v[54:55], v[44:45] neg_lo:[0,1] neg_hi:[0,1]
	v_pk_add_f32 v[54:55], v[86:87], v[58:59]
	v_pk_add_f32 v[58:59], v[86:87], v[58:59] neg_lo:[0,1] neg_hi:[0,1]
	v_xor_b32_e32 v87, 0x80000000, v58
	v_mov_b32_e32 v86, v59
	v_pk_add_f32 v[58:59], v[52:53], v[54:55]
	v_pk_add_f32 v[54:55], v[52:53], v[54:55] neg_lo:[0,1] neg_hi:[0,1]
	v_pk_add_f32 v[52:53], v[60:61], v[82:83]
	v_pk_add_f32 v[60:61], v[60:61], v[82:83] neg_lo:[0,1] neg_hi:[0,1]
	v_pk_add_f32 v[82:83], v[56:57], v[36:37]
	v_pk_add_f32 v[36:37], v[56:57], v[36:37] neg_lo:[0,1] neg_hi:[0,1]
	v_pk_add_f32 v[94:95], v[44:45], v[86:87]
	v_pk_add_f32 v[44:45], v[44:45], v[86:87] neg_lo:[0,1] neg_hi:[0,1]
	v_pk_add_f32 v[86:87], v[52:53], v[82:83]
	v_pk_add_f32 v[52:53], v[52:53], v[82:83] neg_lo:[0,1] neg_hi:[0,1]
	v_pk_add_f32 v[82:83], v[60:61], v[36:37] op_sel:[0,1] op_sel_hi:[1,0] neg_hi:[0,1]
	v_pk_add_f32 v[36:37], v[60:61], v[36:37] op_sel:[0,1] op_sel_hi:[1,0] neg_lo:[0,1]
	v_pk_fma_f32 v[60:61], v[14:15], s[92:93], v[14:15] op_sel:[1,0,0] op_sel_hi:[0,1,1]
	v_pk_mul_f32 v[56:57], v[96:97], s[14:15] op_sel:[1,0] neg_lo:[1,0]
	v_pk_mul_f32 v[90:91], v[60:61], v[88:89] op_sel:[1,1] op_sel_hi:[0,1] neg_lo:[0,1]
	v_pk_fma_f32 v[56:57], v[96:97], s[42:43], v[56:57] op_sel_hi:[0,1,1]
	v_pk_fma_f32 v[88:89], v[60:61], v[88:89], v[90:91] op_sel_hi:[1,0,1]
	ds_write2_b64 v76, v[56:57], v[88:89] offset1:16
	v_pk_mul_f32 v[56:57], v[14:15], v[60:61] op_sel:[1,1] op_sel_hi:[0,1] neg_lo:[0,1]
	v_pk_fma_f32 v[56:57], v[14:15], v[60:61], v[56:57] op_sel_hi:[1,0,1]
	v_pk_mul_f32 v[60:61], v[56:57], v[104:105] op_sel:[1,1] op_sel_hi:[0,1] neg_lo:[0,1]
	v_pk_mul_f32 v[76:77], v[14:15], v[56:57] op_sel:[1,1] op_sel_hi:[0,1] neg_lo:[0,1]
	v_pk_fma_f32 v[60:61], v[56:57], v[104:105], v[60:61] op_sel_hi:[1,0,1]
	v_pk_fma_f32 v[56:57], v[14:15], v[56:57], v[76:77] op_sel_hi:[1,0,1]
	v_pk_mul_f32 v[76:77], v[56:57], v[58:59] op_sel:[1,1] op_sel_hi:[0,1] neg_lo:[0,1]
	v_pk_fma_f32 v[58:59], v[56:57], v[58:59], v[76:77] op_sel_hi:[1,0,1]
	ds_write2_b64 v75, v[60:61], v[58:59] offset0:32 offset1:48
	v_pk_mul_f32 v[58:59], v[14:15], v[56:57] op_sel:[1,1] op_sel_hi:[0,1] neg_lo:[0,1]
	v_pk_fma_f32 v[56:57], v[14:15], v[56:57], v[58:59] op_sel_hi:[1,0,1]
	v_pk_mul_f32 v[58:59], v[56:57], v[106:107] op_sel:[1,1] op_sel_hi:[0,1] neg_lo:[0,1]
	v_pk_mul_f32 v[60:61], v[14:15], v[56:57] op_sel:[1,1] op_sel_hi:[0,1] neg_lo:[0,1]
	v_pk_fma_f32 v[58:59], v[56:57], v[106:107], v[58:59] op_sel_hi:[1,0,1]
	v_pk_fma_f32 v[56:57], v[14:15], v[56:57], v[60:61] op_sel_hi:[1,0,1]
	v_pk_mul_f32 v[60:61], v[56:57], v[84:85] op_sel:[1,1] op_sel_hi:[0,1] neg_lo:[0,1]
	v_pk_fma_f32 v[60:61], v[56:57], v[84:85], v[60:61] op_sel_hi:[1,0,1]
	ds_write2_b64 v74, v[58:59], v[60:61] offset0:64 offset1:80
	v_pk_mul_f32 v[58:59], v[14:15], v[56:57] op_sel:[1,1] op_sel_hi:[0,1] neg_lo:[0,1]
	v_pk_fma_f32 v[56:57], v[14:15], v[56:57], v[58:59] op_sel_hi:[1,0,1]
	v_pk_mul_f32 v[58:59], v[56:57], v[100:101] op_sel:[1,1] op_sel_hi:[0,1] neg_lo:[0,1]
	v_pk_mul_f32 v[60:61], v[14:15], v[56:57] op_sel:[1,1] op_sel_hi:[0,1] neg_lo:[0,1]
	v_pk_fma_f32 v[58:59], v[56:57], v[100:101], v[58:59] op_sel_hi:[1,0,1]
	v_pk_fma_f32 v[56:57], v[14:15], v[56:57], v[60:61] op_sel_hi:[1,0,1]
	v_pk_mul_f32 v[60:61], v[56:57], v[86:87] op_sel:[1,1] op_sel_hi:[0,1] neg_lo:[0,1]
	v_pk_fma_f32 v[60:61], v[56:57], v[86:87], v[60:61] op_sel_hi:[1,0,1]
	ds_write2_b64 v73, v[58:59], v[60:61] offset0:96 offset1:112
	v_pk_mul_f32 v[58:59], v[14:15], v[56:57] op_sel:[1,1] op_sel_hi:[0,1] neg_lo:[0,1]
	v_pk_fma_f32 v[56:57], v[14:15], v[56:57], v[58:59] op_sel_hi:[1,0,1]
	v_pk_mul_f32 v[58:59], v[56:57], v[46:47] op_sel:[1,1] op_sel_hi:[0,1] neg_lo:[0,1]
	v_pk_fma_f32 v[46:47], v[56:57], v[46:47], v[58:59] op_sel_hi:[1,0,1]
	v_pk_mul_f32 v[58:59], v[14:15], v[56:57] op_sel:[1,1] op_sel_hi:[0,1] neg_lo:[0,1]
	v_pk_fma_f32 v[56:57], v[14:15], v[56:57], v[58:59] op_sel_hi:[1,0,1]
	v_pk_mul_f32 v[58:59], v[56:57], v[92:93] op_sel:[1,1] op_sel_hi:[0,1] neg_lo:[0,1]
	v_pk_fma_f32 v[58:59], v[56:57], v[92:93], v[58:59] op_sel_hi:[1,0,1]
	ds_write2_b64 v72, v[46:47], v[58:59] offset0:128 offset1:144
	v_pk_mul_f32 v[46:47], v[14:15], v[56:57] op_sel:[1,1] op_sel_hi:[0,1] neg_lo:[0,1]
	v_pk_fma_f32 v[46:47], v[14:15], v[56:57], v[46:47] op_sel_hi:[1,0,1]
	v_pk_mul_f32 v[56:57], v[46:47], v[50:51] op_sel:[1,1] op_sel_hi:[0,1] neg_lo:[0,1]
	v_pk_fma_f32 v[50:51], v[46:47], v[50:51], v[56:57] op_sel_hi:[1,0,1]
	v_pk_mul_f32 v[56:57], v[14:15], v[46:47] op_sel:[1,1] op_sel_hi:[0,1] neg_lo:[0,1]
	v_pk_fma_f32 v[46:47], v[14:15], v[46:47], v[56:57] op_sel_hi:[1,0,1]
	v_pk_mul_f32 v[56:57], v[46:47], v[94:95] op_sel:[1,1] op_sel_hi:[0,1] neg_lo:[0,1]
	v_pk_fma_f32 v[56:57], v[46:47], v[94:95], v[56:57] op_sel_hi:[1,0,1]
	ds_write2_b64 v71, v[50:51], v[56:57] offset0:160 offset1:176
	v_pk_mul_f32 v[50:51], v[14:15], v[46:47] op_sel:[1,1] op_sel_hi:[0,1] neg_lo:[0,1]
	v_pk_fma_f32 v[46:47], v[14:15], v[46:47], v[50:51] op_sel_hi:[1,0,1]
	v_pk_mul_f32 v[50:51], v[38:39], v[46:47] op_sel:[1,1] op_sel_hi:[1,0] neg_lo:[1,0]
	v_pk_fma_f32 v[38:39], v[38:39], v[46:47], v[50:51] op_sel_hi:[0,1,1]
	v_pk_mul_f32 v[50:51], v[14:15], v[46:47] op_sel:[1,1] op_sel_hi:[0,1] neg_lo:[0,1]
	v_pk_fma_f32 v[46:47], v[14:15], v[46:47], v[50:51] op_sel_hi:[1,0,1]
	v_pk_mul_f32 v[50:51], v[46:47], v[78:79] op_sel:[1,1] op_sel_hi:[0,1] neg_lo:[0,1]
	v_pk_fma_f32 v[50:51], v[46:47], v[78:79], v[50:51] op_sel_hi:[1,0,1]
	ds_write2_b64 v70, v[38:39], v[50:51] offset0:192 offset1:208
	v_pk_mul_f32 v[38:39], v[14:15], v[46:47] op_sel:[1,1] op_sel_hi:[0,1] neg_lo:[0,1]
	v_pk_fma_f32 v[38:39], v[14:15], v[46:47], v[38:39] op_sel_hi:[1,0,1]
	v_pk_mul_f32 v[46:47], v[42:43], v[38:39] op_sel:[1,1] op_sel_hi:[1,0] neg_lo:[1,0]
	v_pk_fma_f32 v[42:43], v[42:43], v[38:39], v[46:47] op_sel_hi:[0,1,1]
	v_pk_mul_f32 v[46:47], v[14:15], v[38:39] op_sel:[1,1] op_sel_hi:[0,1] neg_lo:[0,1]
	v_pk_fma_f32 v[38:39], v[14:15], v[38:39], v[46:47] op_sel_hi:[1,0,1]
	v_pk_mul_f32 v[46:47], v[38:39], v[82:83] op_sel:[1,1] op_sel_hi:[0,1] neg_lo:[0,1]
	v_pk_fma_f32 v[46:47], v[38:39], v[82:83], v[46:47] op_sel_hi:[1,0,1]
	ds_write2_b64 v69, v[42:43], v[46:47] offset0:224 offset1:240
	v_pk_mul_f32 v[42:43], v[14:15], v[38:39] op_sel:[1,1] op_sel_hi:[0,1] neg_lo:[0,1]
	v_pk_fma_f32 v[38:39], v[14:15], v[38:39], v[42:43] op_sel_hi:[1,0,1]
	v_pk_mul_f32 v[42:43], v[30:31], v[38:39] op_sel:[1,1] op_sel_hi:[1,0] neg_lo:[1,0]
	v_pk_fma_f32 v[30:31], v[30:31], v[38:39], v[42:43] op_sel_hi:[0,1,1]
	v_pk_mul_f32 v[42:43], v[14:15], v[38:39] op_sel:[1,1] op_sel_hi:[0,1] neg_lo:[0,1]
	v_pk_fma_f32 v[38:39], v[14:15], v[38:39], v[42:43] op_sel_hi:[1,0,1]
	v_pk_mul_f32 v[42:43], v[80:81], v[38:39] op_sel:[1,1] op_sel_hi:[1,0] neg_lo:[1,0]
	v_pk_fma_f32 v[42:43], v[80:81], v[38:39], v[42:43] op_sel_hi:[0,1,1]
	ds_write2_b64 v68, v[30:31], v[42:43] offset1:16
	v_pk_mul_f32 v[30:31], v[14:15], v[38:39] op_sel:[1,1] op_sel_hi:[0,1] neg_lo:[0,1]
	v_pk_fma_f32 v[30:31], v[14:15], v[38:39], v[30:31] op_sel_hi:[1,0,1]
	v_pk_mul_f32 v[38:39], v[34:35], v[30:31] op_sel:[1,1] op_sel_hi:[1,0] neg_lo:[1,0]
	v_pk_fma_f32 v[34:35], v[34:35], v[30:31], v[38:39] op_sel_hi:[0,1,1]
	v_pk_mul_f32 v[38:39], v[14:15], v[30:31] op_sel:[1,1] op_sel_hi:[0,1] neg_lo:[0,1]
	v_pk_fma_f32 v[30:31], v[14:15], v[30:31], v[38:39] op_sel_hi:[1,0,1]
	v_pk_mul_f32 v[38:39], v[54:55], v[30:31] op_sel:[1,1] op_sel_hi:[1,0] neg_lo:[1,0]
	v_pk_fma_f32 v[38:39], v[54:55], v[30:31], v[38:39] op_sel_hi:[0,1,1]
	ds_write2_b64 v67, v[34:35], v[38:39] offset0:32 offset1:48
	v_pk_mul_f32 v[34:35], v[14:15], v[30:31] op_sel:[1,1] op_sel_hi:[0,1] neg_lo:[0,1]
	v_pk_fma_f32 v[30:31], v[14:15], v[30:31], v[34:35] op_sel_hi:[1,0,1]
	v_pk_mul_f32 v[34:35], v[26:27], v[30:31] op_sel:[1,1] op_sel_hi:[1,0] neg_lo:[1,0]
	v_pk_fma_f32 v[26:27], v[26:27], v[30:31], v[34:35] op_sel_hi:[0,1,1]
	v_pk_mul_f32 v[34:35], v[14:15], v[30:31] op_sel:[1,1] op_sel_hi:[0,1] neg_lo:[0,1]
	v_pk_fma_f32 v[30:31], v[14:15], v[30:31], v[34:35] op_sel_hi:[1,0,1]
	v_pk_mul_f32 v[34:35], v[48:49], v[30:31] op_sel:[1,1] op_sel_hi:[1,0] neg_lo:[1,0]
	v_pk_fma_f32 v[34:35], v[48:49], v[30:31], v[34:35] op_sel_hi:[0,1,1]
	ds_write2_b64 v66, v[26:27], v[34:35] offset0:64 offset1:80
	v_pk_mul_f32 v[26:27], v[14:15], v[30:31] op_sel:[1,1] op_sel_hi:[0,1] neg_lo:[0,1]
	v_pk_fma_f32 v[26:27], v[14:15], v[30:31], v[26:27] op_sel_hi:[1,0,1]
	v_pk_mul_f32 v[30:31], v[28:29], v[26:27] op_sel:[1,1] op_sel_hi:[1,0] neg_lo:[1,0]
	v_pk_fma_f32 v[28:29], v[28:29], v[26:27], v[30:31] op_sel_hi:[0,1,1]
	v_pk_mul_f32 v[30:31], v[14:15], v[26:27] op_sel:[1,1] op_sel_hi:[0,1] neg_lo:[0,1]
	v_pk_fma_f32 v[26:27], v[14:15], v[26:27], v[30:31] op_sel_hi:[1,0,1]
	v_pk_mul_f32 v[30:31], v[52:53], v[26:27] op_sel:[1,1] op_sel_hi:[1,0] neg_lo:[1,0]
	v_pk_fma_f32 v[30:31], v[52:53], v[26:27], v[30:31] op_sel_hi:[0,1,1]
	ds_write2_b64 v65, v[28:29], v[30:31] offset0:96 offset1:112
	v_pk_mul_f32 v[28:29], v[14:15], v[26:27] op_sel:[1,1] op_sel_hi:[0,1] neg_lo:[0,1]
	v_pk_fma_f32 v[26:27], v[14:15], v[26:27], v[28:29] op_sel_hi:[1,0,1]
	v_pk_mul_f32 v[28:29], v[22:23], v[26:27] op_sel:[1,1] op_sel_hi:[1,0] neg_lo:[1,0]
	v_pk_fma_f32 v[22:23], v[22:23], v[26:27], v[28:29] op_sel_hi:[0,1,1]
	v_pk_mul_f32 v[28:29], v[14:15], v[26:27] op_sel:[1,1] op_sel_hi:[0,1] neg_lo:[0,1]
	v_pk_fma_f32 v[26:27], v[14:15], v[26:27], v[28:29] op_sel_hi:[1,0,1]
	v_pk_mul_f32 v[28:29], v[40:41], v[26:27] op_sel:[1,1] op_sel_hi:[1,0] neg_lo:[1,0]
	v_pk_fma_f32 v[28:29], v[40:41], v[26:27], v[28:29] op_sel_hi:[0,1,1]
	ds_write2_b64 v64, v[22:23], v[28:29] offset0:128 offset1:144
	v_pk_mul_f32 v[22:23], v[14:15], v[26:27] op_sel:[1,1] op_sel_hi:[0,1] neg_lo:[0,1]
	v_pk_fma_f32 v[22:23], v[14:15], v[26:27], v[22:23] op_sel_hi:[1,0,1]
	v_pk_mul_f32 v[26:27], v[24:25], v[22:23] op_sel:[1,1] op_sel_hi:[1,0] neg_lo:[1,0]
	v_pk_fma_f32 v[24:25], v[24:25], v[22:23], v[26:27] op_sel_hi:[0,1,1]
	v_pk_mul_f32 v[26:27], v[14:15], v[22:23] op_sel:[1,1] op_sel_hi:[0,1] neg_lo:[0,1]
	v_pk_fma_f32 v[22:23], v[14:15], v[22:23], v[26:27] op_sel_hi:[1,0,1]
	v_pk_mul_f32 v[26:27], v[44:45], v[22:23] op_sel:[1,1] op_sel_hi:[1,0] neg_lo:[1,0]
	v_pk_fma_f32 v[26:27], v[44:45], v[22:23], v[26:27] op_sel_hi:[0,1,1]
	ds_write2_b64 v63, v[24:25], v[26:27] offset0:160 offset1:176
	v_pk_mul_f32 v[24:25], v[14:15], v[22:23] op_sel:[1,1] op_sel_hi:[0,1] neg_lo:[0,1]
	v_pk_fma_f32 v[22:23], v[14:15], v[22:23], v[24:25] op_sel_hi:[1,0,1]
	v_pk_mul_f32 v[24:25], v[18:19], v[22:23] op_sel:[1,1] op_sel_hi:[1,0] neg_lo:[1,0]
	v_pk_fma_f32 v[18:19], v[18:19], v[22:23], v[24:25] op_sel_hi:[0,1,1]
	v_pk_mul_f32 v[24:25], v[14:15], v[22:23] op_sel:[1,1] op_sel_hi:[0,1] neg_lo:[0,1]
	v_pk_fma_f32 v[22:23], v[14:15], v[22:23], v[24:25] op_sel_hi:[1,0,1]
	v_pk_mul_f32 v[24:25], v[32:33], v[22:23] op_sel:[1,1] op_sel_hi:[1,0] neg_lo:[1,0]
	v_pk_fma_f32 v[24:25], v[32:33], v[22:23], v[24:25] op_sel_hi:[0,1,1]
	ds_write2_b64 v62, v[18:19], v[24:25] offset0:192 offset1:208
	v_pk_mul_f32 v[18:19], v[14:15], v[22:23] op_sel:[1,1] op_sel_hi:[0,1] neg_lo:[0,1]
	v_pk_fma_f32 v[18:19], v[14:15], v[22:23], v[18:19] op_sel_hi:[1,0,1]
	v_pk_mul_f32 v[22:23], v[20:21], v[18:19] op_sel:[1,1] op_sel_hi:[1,0] neg_lo:[1,0]
	v_pk_fma_f32 v[20:21], v[20:21], v[18:19], v[22:23] op_sel_hi:[0,1,1]
	v_pk_mul_f32 v[22:23], v[14:15], v[18:19] op_sel:[1,1] op_sel_hi:[0,1] neg_lo:[0,1]
	v_pk_fma_f32 v[14:15], v[14:15], v[18:19], v[22:23] op_sel_hi:[1,0,1]
	v_pk_mul_f32 v[18:19], v[36:37], v[14:15] op_sel:[1,1] op_sel_hi:[1,0] neg_lo:[1,0]
	v_pk_fma_f32 v[14:15], v[36:37], v[14:15], v[18:19] op_sel_hi:[0,1,1]
	ds_write2_b64 v13, v[20:21], v[14:15] offset0:224 offset1:240
	v_mov_b32_e32 v14, v1
	v_mov_b32_e32 v10, v178
	v_mov_b32_e32 v13, v177
	s_waitcnt lgkmcnt(0)
	s_barrier
	v_mov_b32_e32 v50, v168
	v_xor_b32_e32 v18, 1, v13
	v_lshlrev_b32_e32 v10, 3, v10
	v_lshlrev_b32_e32 v18, 3, v18
	v_add3_u32 v20, 0, v18, v10
	v_xor_b32_e32 v18, 2, v13
	v_lshlrev_b32_e32 v18, 3, v18
	v_xor_b32_e32 v26, 5, v13
	v_add3_u32 v22, 0, v18, v10
	v_xor_b32_e32 v18, 3, v13
	v_lshlrev_b32_e32 v26, 3, v26
	v_lshlrev_b32_e32 v15, 3, v13
	v_lshlrev_b32_e32 v18, 3, v18
	v_add3_u32 v28, 0, v26, v10
	v_xor_b32_e32 v26, 6, v13
	v_add3_u32 v15, 0, v15, v10
	v_add3_u32 v24, 0, v18, v10
	v_lshlrev_b32_e32 v26, 3, v26
	v_xor_b32_e32 v34, 9, v13
	ds_read_b64 v[18:19], v15
	ds_read_b64 v[20:21], v20
	ds_read_b64 v[22:23], v22
	ds_read_b64 v[24:25], v24
	v_xor_b32_e32 v15, 4, v13
	v_add3_u32 v30, 0, v26, v10
	v_xor_b32_e32 v26, 7, v13
	v_lshlrev_b32_e32 v34, 3, v34
	v_lshlrev_b32_e32 v15, 3, v15
	v_lshlrev_b32_e32 v26, 3, v26
	v_add3_u32 v36, 0, v34, v10
	v_xor_b32_e32 v34, 10, v13
	v_add3_u32 v15, 0, v15, v10
	v_add3_u32 v32, 0, v26, v10
	v_lshlrev_b32_e32 v34, 3, v34
	ds_read_b64 v[26:27], v15
	ds_read_b64 v[28:29], v28
	ds_read_b64 v[30:31], v30
	ds_read_b64 v[32:33], v32
	v_xor_b32_e32 v15, 8, v13
	v_add3_u32 v38, 0, v34, v10
	v_xor_b32_e32 v34, 11, v13
	v_lshlrev_b32_e32 v15, 3, v15
	v_lshlrev_b32_e32 v34, 3, v34
	v_xor_b32_e32 v42, 13, v13
	v_add3_u32 v15, 0, v15, v10
	v_add3_u32 v40, 0, v34, v10
	v_lshlrev_b32_e32 v42, 3, v42
	ds_read_b64 v[34:35], v15
	ds_read_b64 v[36:37], v36
	ds_read_b64 v[38:39], v38
	ds_read_b64 v[40:41], v40
	v_xor_b32_e32 v15, 12, v13
	v_add3_u32 v44, 0, v42, v10
	v_xor_b32_e32 v42, 14, v13
	v_xor_b32_e32 v13, 15, v13
	v_lshlrev_b32_e32 v15, 3, v15
	v_lshlrev_b32_e32 v42, 3, v42
	v_lshlrev_b32_e32 v13, 3, v13
	v_add3_u32 v15, 0, v15, v10
	v_add3_u32 v46, 0, v42, v10
	v_add3_u32 v10, 0, v13, v10
	ds_read_b64 v[42:43], v15
	ds_read_b64 v[44:45], v44
	ds_read_b64 v[46:47], v46
	ds_read_b64 v[48:49], v10
	v_mov_b32_e32 v10, v164
	v_mov_b32_e32 v13, v167
	v_mov_b32_e32 v10, v165
	s_waitcnt lgkmcnt(7)
	v_pk_add_f32 v[54:55], v[18:19], v[34:35]
	v_mov_b32_e32 v10, v166
	v_pk_add_f32 v[18:19], v[18:19], v[34:35] neg_lo:[0,1] neg_hi:[0,1]
	s_waitcnt lgkmcnt(6)
	v_pk_add_f32 v[34:35], v[20:21], v[36:37]
	v_pk_add_f32 v[20:21], v[20:21], v[36:37] neg_lo:[0,1] neg_hi:[0,1]
	v_mov_b32_e32 v13, v169
	v_mov_b32_e32 v52, v170
	v_ashrrev_i32_e32 v15, 31, v14
	v_pk_mul_f32 v[36:37], v[20:21], v[52:53] op_sel:[1,0] op_sel_hi:[0,0] neg_lo:[1,1] neg_hi:[0,1]
	v_mov_b32_e32 v13, v171
	v_pk_fma_f32 v[20:21], v[20:21], v[10:11], v[36:37] op_sel_hi:[1,0,1]
	s_waitcnt lgkmcnt(5)
	v_pk_add_f32 v[36:37], v[22:23], v[38:39]
	v_pk_add_f32 v[22:23], v[22:23], v[38:39] neg_lo:[0,1] neg_hi:[0,1]
	s_movk_i32 s85, 0x1000
	v_pk_mul_f32 v[38:39], v[22:23], v[50:51] op_sel:[1,0] op_sel_hi:[0,0] neg_lo:[1,1] neg_hi:[0,1]
	v_mov_b32_e32 v13, v172
	v_pk_fma_f32 v[22:23], v[22:23], v[50:51], v[38:39] op_sel_hi:[1,0,1]
	s_waitcnt lgkmcnt(4)
	v_pk_add_f32 v[38:39], v[24:25], v[40:41]
	v_pk_add_f32 v[24:25], v[24:25], v[40:41] neg_lo:[0,1] neg_hi:[0,1]
	s_movk_i32 s84, 0x2000
	v_pk_mul_f32 v[40:41], v[24:25], v[52:53] op_sel_hi:[1,0]
	v_pk_fma_f32 v[24:25], v[24:25], v[10:11], v[40:41] op_sel:[1,0,0] op_sel_hi:[0,0,1] neg_lo:[1,1,0] neg_hi:[0,1,0]
	s_waitcnt lgkmcnt(3)
	v_pk_add_f32 v[40:41], v[26:27], v[42:43]
	v_pk_add_f32 v[26:27], v[26:27], v[42:43] neg_lo:[0,1] neg_hi:[0,1]
	v_mov_b32_e32 v13, v177
	v_xor_b32_e32 v43, 0x80000000, v26
	v_mov_b32_e32 v42, v27
	s_waitcnt lgkmcnt(2)
	v_pk_add_f32 v[26:27], v[28:29], v[44:45]
	v_pk_add_f32 v[28:29], v[28:29], v[44:45] neg_lo:[0,1] neg_hi:[0,1]
	s_movk_i32 s88, 0x6000
	v_pk_mul_f32 v[44:45], v[28:29], v[52:53] op_sel_hi:[1,0] neg_lo:[0,1] neg_hi:[0,1]
	v_pk_fma_f32 v[28:29], v[28:29], v[10:11], v[44:45] op_sel:[1,0,0] op_sel_hi:[0,0,1] neg_lo:[1,1,0] neg_hi:[0,1,0]
	s_waitcnt lgkmcnt(1)
	v_pk_add_f32 v[44:45], v[30:31], v[46:47]
	v_pk_add_f32 v[30:31], v[30:31], v[46:47] neg_lo:[0,1] neg_hi:[0,1]
	s_mov_b32 s0, 0x8000
	v_pk_mul_f32 v[46:47], v[30:31], v[50:51] op_sel:[1,0] op_sel_hi:[0,0] neg_lo:[1,1] neg_hi:[0,1]
	s_movk_i32 s86, 0x5000
	v_pk_fma_f32 v[30:31], v[30:31], v[50:51], v[46:47] op_sel_hi:[1,0,1] neg_lo:[0,1,0] neg_hi:[0,1,0]
	s_waitcnt lgkmcnt(0)
	v_pk_add_f32 v[46:47], v[32:33], v[48:49]
	v_pk_add_f32 v[32:33], v[32:33], v[48:49] neg_lo:[0,1] neg_hi:[0,1]
	v_mov_b32_e32 v72, v165
	v_pk_mul_f32 v[48:49], v[32:33], v[52:53] op_sel:[1,0] op_sel_hi:[0,0] neg_lo:[1,1] neg_hi:[0,1]
	v_pk_add_f32 v[52:53], v[34:35], v[26:27]
	v_pk_add_f32 v[26:27], v[34:35], v[26:27] neg_lo:[0,1] neg_hi:[0,1]
	v_pk_fma_f32 v[32:33], v[32:33], v[10:11], v[48:49] op_sel_hi:[1,0,1] neg_lo:[0,1,0] neg_hi:[0,1,0]
	v_pk_mul_f32 v[34:35], v[26:27], v[50:51] op_sel:[1,0] op_sel_hi:[0,0] neg_lo:[1,1] neg_hi:[0,1]
	v_pk_add_f32 v[48:49], v[54:55], v[40:41]
	v_pk_fma_f32 v[26:27], v[26:27], v[50:51], v[34:35] op_sel_hi:[1,0,1]
	v_pk_add_f32 v[34:35], v[36:37], v[44:45]
	v_pk_add_f32 v[36:37], v[36:37], v[44:45] neg_lo:[0,1] neg_hi:[0,1]
	v_pk_add_f32 v[40:41], v[54:55], v[40:41] neg_lo:[0,1] neg_hi:[0,1]
	v_xor_b32_e32 v45, 0x80000000, v36
	v_mov_b32_e32 v44, v37
	v_pk_add_f32 v[36:37], v[38:39], v[46:47]
	v_pk_add_f32 v[38:39], v[38:39], v[46:47] neg_lo:[0,1] neg_hi:[0,1]
	v_mov_b32_e32 v10, v179
	v_pk_mul_f32 v[46:47], v[38:39], v[50:51] op_sel:[1,0] op_sel_hi:[0,0] neg_lo:[1,1] neg_hi:[0,1]
	v_mov_b32_e32 v74, v167
	v_pk_fma_f32 v[38:39], v[38:39], v[50:51], v[46:47] op_sel_hi:[1,0,1] neg_lo:[0,1,0] neg_hi:[0,1,0]
	v_pk_add_f32 v[46:47], v[48:49], v[34:35]
	v_pk_add_f32 v[34:35], v[48:49], v[34:35] neg_lo:[0,1] neg_hi:[0,1]
	v_pk_add_f32 v[48:49], v[52:53], v[36:37]
	v_pk_add_f32 v[36:37], v[52:53], v[36:37] neg_lo:[0,1] neg_hi:[0,1]
	v_mov_b32_e32 v76, v169
	v_xor_b32_e32 v53, 0x80000000, v36
	v_mov_b32_e32 v52, v37
	v_pk_add_f32 v[36:37], v[46:47], v[48:49]
	v_pk_add_f32 v[46:47], v[46:47], v[48:49] neg_lo:[0,1] neg_hi:[0,1]
	v_pk_add_f32 v[48:49], v[34:35], v[52:53]
	v_pk_add_f32 v[34:35], v[34:35], v[52:53] neg_lo:[0,1] neg_hi:[0,1]
	v_pk_add_f32 v[52:53], v[40:41], v[44:45]
	v_pk_add_f32 v[40:41], v[40:41], v[44:45] neg_lo:[0,1] neg_hi:[0,1]
	v_pk_add_f32 v[44:45], v[26:27], v[38:39]
	v_pk_add_f32 v[26:27], v[26:27], v[38:39] neg_lo:[0,1] neg_hi:[0,1]
	v_mov_b32_e32 v78, v171
	v_xor_b32_e32 v39, 0x80000000, v26
	v_mov_b32_e32 v38, v27
	v_pk_add_f32 v[26:27], v[52:53], v[44:45]
	v_pk_add_f32 v[44:45], v[52:53], v[44:45] neg_lo:[0,1] neg_hi:[0,1]
	v_pk_add_f32 v[52:53], v[40:41], v[38:39]
	v_pk_add_f32 v[38:39], v[40:41], v[38:39] neg_lo:[0,1] neg_hi:[0,1]
	v_pk_add_f32 v[40:41], v[18:19], v[42:43]
	v_pk_add_f32 v[18:19], v[18:19], v[42:43] neg_lo:[0,1] neg_hi:[0,1]
	v_pk_add_f32 v[42:43], v[20:21], v[28:29]
	v_pk_add_f32 v[20:21], v[20:21], v[28:29] neg_lo:[0,1] neg_hi:[0,1]
	v_mov_b32_e32 v83, v11
	v_pk_mul_f32 v[28:29], v[50:51], v[20:21] op_sel:[0,1] op_sel_hi:[0,0] neg_lo:[1,1] neg_hi:[1,0]
	v_pk_fma_f32 v[20:21], v[50:51], v[20:21], v[28:29] op_sel_hi:[0,1,1]
	v_pk_add_f32 v[28:29], v[22:23], v[30:31]
	v_pk_add_f32 v[22:23], v[22:23], v[30:31] neg_lo:[0,1] neg_hi:[0,1]
	s_mov_b32 s1, 0xe000
	v_xor_b32_e32 v31, 0x80000000, v22
	v_mov_b32_e32 v30, v23
	v_pk_add_f32 v[22:23], v[24:25], v[32:33]
	v_pk_add_f32 v[24:25], v[24:25], v[32:33] neg_lo:[0,1] neg_hi:[0,1]
	s_mov_b32 s8, 0x8000
	v_pk_mul_f32 v[32:33], v[50:51], v[24:25] op_sel:[0,1] op_sel_hi:[0,0] neg_lo:[1,1] neg_hi:[1,0]
	v_pk_fma_f32 v[24:25], v[50:51], v[24:25], v[32:33] op_sel_hi:[0,1,1] neg_lo:[1,0,0] neg_hi:[1,0,0]
	v_pk_add_f32 v[32:33], v[40:41], v[28:29]
	v_pk_add_f32 v[28:29], v[40:41], v[28:29] neg_lo:[0,1] neg_hi:[0,1]
	v_pk_add_f32 v[40:41], v[42:43], v[22:23]
	v_pk_add_f32 v[22:23], v[42:43], v[22:23] neg_lo:[0,1] neg_hi:[0,1]
	v_mov_b32_e32 v50, v168
	v_xor_b32_e32 v43, 0x80000000, v22
	v_mov_b32_e32 v42, v23
	v_pk_add_f32 v[22:23], v[32:33], v[40:41]
	v_pk_add_f32 v[32:33], v[32:33], v[40:41] neg_lo:[0,1] neg_hi:[0,1]
	v_pk_add_f32 v[40:41], v[28:29], v[42:43]
	v_pk_add_f32 v[28:29], v[28:29], v[42:43] neg_lo:[0,1] neg_hi:[0,1]
	v_pk_add_f32 v[42:43], v[18:19], v[30:31]
	v_pk_add_f32 v[18:19], v[18:19], v[30:31] neg_lo:[0,1] neg_hi:[0,1]
	v_pk_add_f32 v[30:31], v[20:21], v[24:25]
	v_pk_add_f32 v[20:21], v[20:21], v[24:25] neg_lo:[0,1] neg_hi:[0,1]
	s_mov_b32 s7, 0xa000
	v_xor_b32_e32 v25, 0x80000000, v20
	v_mov_b32_e32 v24, v21
	v_pk_add_f32 v[20:21], v[42:43], v[30:31]
	v_pk_add_f32 v[30:31], v[42:43], v[30:31] neg_lo:[0,1] neg_hi:[0,1]
	v_pk_add_f32 v[42:43], v[18:19], v[24:25]
	v_pk_add_f32 v[18:19], v[18:19], v[24:25] neg_lo:[0,1] neg_hi:[0,1]
	v_lshl_add_u64 v[24:25], v[14:15], 3, s[48:49]
	global_store_dwordx2 v[24:25], v[36:37], off
	v_add_u32_e32 v24, 0x200, v14
	v_ashrrev_i32_e32 v25, 31, v24
	v_lshl_add_u64 v[24:25], v[24:25], 3, s[48:49]
	global_store_dwordx2 v[24:25], v[22:23], off
	v_add_u32_e32 v22, 0x400, v14
	v_ashrrev_i32_e32 v23, 31, v22
	v_lshl_add_u64 v[22:23], v[22:23], 3, s[48:49]
	global_store_dwordx2 v[22:23], v[26:27], off
	v_add_u32_e32 v22, 0x600, v14
	v_ashrrev_i32_e32 v23, 31, v22
	v_lshl_add_u64 v[22:23], v[22:23], 3, s[48:49]
	global_store_dwordx2 v[22:23], v[20:21], off
	v_add_u32_e32 v20, 0x800, v14
	v_ashrrev_i32_e32 v21, 31, v20
	v_lshl_add_u64 v[20:21], v[20:21], 3, s[48:49]
	global_store_dwordx2 v[20:21], v[48:49], off
	v_add_u32_e32 v20, 0xa00, v14
	v_ashrrev_i32_e32 v21, 31, v20
	v_lshl_add_u64 v[20:21], v[20:21], 3, s[48:49]
	global_store_dwordx2 v[20:21], v[40:41], off
	v_add_u32_e32 v20, 0xc00, v14
	v_ashrrev_i32_e32 v21, 31, v20
	v_lshl_add_u64 v[20:21], v[20:21], 3, s[48:49]
	global_store_dwordx2 v[20:21], v[52:53], off
	v_add_u32_e32 v20, 0xe00, v14
	v_ashrrev_i32_e32 v21, 31, v20
	v_lshl_add_u64 v[20:21], v[20:21], 3, s[48:49]
	global_store_dwordx2 v[20:21], v[42:43], off
	v_add_u32_e32 v20, 0x1000, v14
	v_ashrrev_i32_e32 v21, 31, v20
	v_lshl_add_u64 v[20:21], v[20:21], 3, s[48:49]
	global_store_dwordx2 v[20:21], v[46:47], off
	v_add_u32_e32 v20, 0x1200, v14
	v_ashrrev_i32_e32 v21, 31, v20
	v_lshl_add_u64 v[20:21], v[20:21], 3, s[48:49]
	global_store_dwordx2 v[20:21], v[32:33], off
	v_add_u32_e32 v20, 0x1400, v14
	v_ashrrev_i32_e32 v21, 31, v20
	v_lshl_add_u64 v[20:21], v[20:21], 3, s[48:49]
	global_store_dwordx2 v[20:21], v[44:45], off
	v_add_u32_e32 v20, 0x1600, v14
	v_ashrrev_i32_e32 v21, 31, v20
	v_lshl_add_u64 v[20:21], v[20:21], 3, s[48:49]
	global_store_dwordx2 v[20:21], v[30:31], off
	v_add_u32_e32 v20, 0x1800, v14
	v_ashrrev_i32_e32 v21, 31, v20
	v_lshl_add_u64 v[20:21], v[20:21], 3, s[48:49]
	global_store_dwordx2 v[20:21], v[34:35], off
	v_add_u32_e32 v20, 0x1a00, v14
	v_ashrrev_i32_e32 v21, 31, v20
	v_lshl_add_u64 v[20:21], v[20:21], 3, s[48:49]
	global_store_dwordx2 v[20:21], v[28:29], off
	v_add_u32_e32 v20, 0x1c00, v14
	v_ashrrev_i32_e32 v21, 31, v20
	v_lshl_add_u64 v[20:21], v[20:21], 3, s[48:49]
	global_store_dwordx2 v[20:21], v[38:39], off
	v_add_u32_e32 v20, 0x1e00, v14
	v_ashrrev_i32_e32 v21, 31, v20
	v_lshl_add_u64 v[20:21], v[20:21], 3, s[48:49]
	global_store_dwordx2 v[20:21], v[18:19], off
	v_mov_b32_e32 v52, v170
	v_xor_b32_e32 v18, 1, v13
	v_lshlrev_b32_e32 v10, 3, v10
	v_lshlrev_b32_e32 v18, 3, v18
	v_add3_u32 v20, 0, v18, v10
	v_xor_b32_e32 v18, 2, v13
	v_lshlrev_b32_e32 v18, 3, v18
	v_xor_b32_e32 v26, 5, v13
	v_add3_u32 v22, 0, v18, v10
	v_xor_b32_e32 v18, 3, v13
	v_lshlrev_b32_e32 v26, 3, v26
	v_lshlrev_b32_e32 v15, 3, v13
	v_lshlrev_b32_e32 v18, 3, v18
	v_add3_u32 v28, 0, v26, v10
	v_xor_b32_e32 v26, 6, v13
	v_add3_u32 v15, 0, v15, v10
	v_add3_u32 v24, 0, v18, v10
	v_lshlrev_b32_e32 v26, 3, v26
	v_xor_b32_e32 v34, 9, v13
	ds_read_b64 v[18:19], v15
	ds_read_b64 v[20:21], v20
	ds_read_b64 v[22:23], v22
	ds_read_b64 v[24:25], v24
	v_xor_b32_e32 v15, 4, v13
	v_add3_u32 v30, 0, v26, v10
	v_xor_b32_e32 v26, 7, v13
	v_lshlrev_b32_e32 v34, 3, v34
	v_lshlrev_b32_e32 v15, 3, v15
	v_lshlrev_b32_e32 v26, 3, v26
	v_add3_u32 v36, 0, v34, v10
	v_xor_b32_e32 v34, 10, v13
	v_add3_u32 v15, 0, v15, v10
	v_add3_u32 v32, 0, v26, v10
	v_lshlrev_b32_e32 v34, 3, v34
	ds_read_b64 v[26:27], v15
	ds_read_b64 v[28:29], v28
	ds_read_b64 v[30:31], v30
	ds_read_b64 v[32:33], v32
	v_xor_b32_e32 v15, 8, v13
	v_add3_u32 v38, 0, v34, v10
	v_xor_b32_e32 v34, 11, v13
	v_lshlrev_b32_e32 v15, 3, v15
	v_lshlrev_b32_e32 v34, 3, v34
	v_xor_b32_e32 v42, 13, v13
	v_add3_u32 v15, 0, v15, v10
	v_add3_u32 v40, 0, v34, v10
	v_lshlrev_b32_e32 v42, 3, v42
	ds_read_b64 v[34:35], v15
	ds_read_b64 v[36:37], v36
	ds_read_b64 v[38:39], v38
	ds_read_b64 v[40:41], v40
	v_xor_b32_e32 v15, 12, v13
	v_add3_u32 v44, 0, v42, v10
	v_xor_b32_e32 v42, 14, v13
	v_xor_b32_e32 v13, 15, v13
	v_lshlrev_b32_e32 v15, 3, v15
	v_lshlrev_b32_e32 v42, 3, v42
	v_lshlrev_b32_e32 v13, 3, v13
	v_add3_u32 v15, 0, v15, v10
	v_add3_u32 v46, 0, v42, v10
	v_add3_u32 v10, 0, v13, v10
	ds_read_b64 v[42:43], v15
	ds_read_b64 v[44:45], v44
	ds_read_b64 v[46:47], v46
	ds_read_b64 v[48:49], v10
	v_mov_b32_e32 v10, v164
	v_mov_b32_e32 v13, v167
	v_mov_b32_e32 v10, v165
	s_waitcnt lgkmcnt(7)
	v_pk_add_f32 v[54:55], v[18:19], v[34:35]
	v_mov_b32_e32 v10, v166
	v_pk_add_f32 v[18:19], v[18:19], v[34:35] neg_lo:[0,1] neg_hi:[0,1]
	s_waitcnt lgkmcnt(6)
	v_pk_add_f32 v[34:35], v[20:21], v[36:37]
	v_pk_add_f32 v[20:21], v[20:21], v[36:37] neg_lo:[0,1] neg_hi:[0,1]
	v_mov_b32_e32 v13, v169
	s_mov_b32 s9, 0x9000
	v_pk_mul_f32 v[36:37], v[20:21], v[52:53] op_sel:[1,0] op_sel_hi:[0,0] neg_lo:[1,1] neg_hi:[0,1]
	v_mov_b32_e32 v13, v171
	v_pk_fma_f32 v[20:21], v[20:21], v[10:11], v[36:37] op_sel_hi:[1,0,1]
	s_waitcnt lgkmcnt(5)
	v_pk_add_f32 v[36:37], v[22:23], v[38:39]
	v_pk_add_f32 v[22:23], v[22:23], v[38:39] neg_lo:[0,1] neg_hi:[0,1]
	s_mov_b32 s5, 0xb000
	v_pk_mul_f32 v[38:39], v[22:23], v[50:51] op_sel:[1,0] op_sel_hi:[0,0] neg_lo:[1,1] neg_hi:[0,1]
	v_mov_b32_e32 v13, v172
	v_pk_fma_f32 v[22:23], v[22:23], v[50:51], v[38:39] op_sel_hi:[1,0,1]
	s_waitcnt lgkmcnt(4)
	v_pk_add_f32 v[38:39], v[24:25], v[40:41]
	v_pk_add_f32 v[24:25], v[24:25], v[40:41] neg_lo:[0,1] neg_hi:[0,1]
	s_mov_b32 s6, 0xc000
	v_pk_mul_f32 v[40:41], v[24:25], v[52:53] op_sel_hi:[1,0]
	v_pk_fma_f32 v[24:25], v[24:25], v[10:11], v[40:41] op_sel:[1,0,0] op_sel_hi:[0,0,1] neg_lo:[1,1,0] neg_hi:[0,1,0]
	s_waitcnt lgkmcnt(3)
	v_pk_add_f32 v[40:41], v[26:27], v[42:43]
	v_pk_add_f32 v[26:27], v[26:27], v[42:43] neg_lo:[0,1] neg_hi:[0,1]
	s_mov_b32 s4, 0xd000
	v_xor_b32_e32 v43, 0x80000000, v26
	v_mov_b32_e32 v42, v27
	s_waitcnt lgkmcnt(2)
	v_pk_add_f32 v[26:27], v[28:29], v[44:45]
	v_pk_add_f32 v[28:29], v[28:29], v[44:45] neg_lo:[0,1] neg_hi:[0,1]
	v_pk_mul_f32 v[44:45], v[28:29], v[52:53] op_sel_hi:[1,0] neg_lo:[0,1] neg_hi:[0,1]
	v_pk_fma_f32 v[28:29], v[28:29], v[10:11], v[44:45] op_sel:[1,0,0] op_sel_hi:[0,0,1] neg_lo:[1,1,0] neg_hi:[0,1,0]
	s_waitcnt lgkmcnt(1)
	v_pk_add_f32 v[44:45], v[30:31], v[46:47]
	v_pk_add_f32 v[30:31], v[30:31], v[46:47] neg_lo:[0,1] neg_hi:[0,1]
	v_pk_mul_f32 v[46:47], v[30:31], v[50:51] op_sel:[1,0] op_sel_hi:[0,0] neg_lo:[1,1] neg_hi:[0,1]
	v_pk_fma_f32 v[30:31], v[30:31], v[50:51], v[46:47] op_sel_hi:[1,0,1] neg_lo:[0,1,0] neg_hi:[0,1,0]
	s_waitcnt lgkmcnt(0)
	v_pk_add_f32 v[46:47], v[32:33], v[48:49]
	v_pk_add_f32 v[32:33], v[32:33], v[48:49] neg_lo:[0,1] neg_hi:[0,1]
	v_pk_mul_f32 v[48:49], v[32:33], v[52:53] op_sel:[1,0] op_sel_hi:[0,0] neg_lo:[1,1] neg_hi:[0,1]
	v_pk_add_f32 v[52:53], v[34:35], v[26:27]
	v_pk_add_f32 v[26:27], v[34:35], v[26:27] neg_lo:[0,1] neg_hi:[0,1]
	v_pk_fma_f32 v[32:33], v[32:33], v[10:11], v[48:49] op_sel_hi:[1,0,1] neg_lo:[0,1,0] neg_hi:[0,1,0]
	v_pk_mul_f32 v[34:35], v[26:27], v[50:51] op_sel:[1,0] op_sel_hi:[0,0] neg_lo:[1,1] neg_hi:[0,1]
	v_pk_add_f32 v[48:49], v[54:55], v[40:41]
	v_pk_fma_f32 v[26:27], v[26:27], v[50:51], v[34:35] op_sel_hi:[1,0,1]
	v_pk_add_f32 v[34:35], v[36:37], v[44:45]
	v_pk_add_f32 v[36:37], v[36:37], v[44:45] neg_lo:[0,1] neg_hi:[0,1]
	v_pk_add_f32 v[40:41], v[54:55], v[40:41] neg_lo:[0,1] neg_hi:[0,1]
	v_xor_b32_e32 v45, 0x80000000, v36
	v_mov_b32_e32 v44, v37
	v_pk_add_f32 v[36:37], v[38:39], v[46:47]
	v_pk_add_f32 v[38:39], v[38:39], v[46:47] neg_lo:[0,1] neg_hi:[0,1]
	v_mov_b32_e32 v10, v164
	v_pk_mul_f32 v[46:47], v[38:39], v[50:51] op_sel:[1,0] op_sel_hi:[0,0] neg_lo:[1,1] neg_hi:[0,1]
	v_pk_fma_f32 v[38:39], v[38:39], v[50:51], v[46:47] op_sel_hi:[1,0,1] neg_lo:[0,1,0] neg_hi:[0,1,0]
	v_pk_add_f32 v[46:47], v[48:49], v[34:35]
	v_pk_add_f32 v[34:35], v[48:49], v[34:35] neg_lo:[0,1] neg_hi:[0,1]
	v_pk_add_f32 v[48:49], v[52:53], v[36:37]
	v_pk_add_f32 v[36:37], v[52:53], v[36:37] neg_lo:[0,1] neg_hi:[0,1]
	v_xor_b32_e32 v53, 0x80000000, v36
	v_mov_b32_e32 v52, v37
	v_pk_add_f32 v[36:37], v[46:47], v[48:49]
	v_pk_add_f32 v[46:47], v[46:47], v[48:49] neg_lo:[0,1] neg_hi:[0,1]
	v_pk_add_f32 v[48:49], v[34:35], v[52:53]
	v_pk_add_f32 v[34:35], v[34:35], v[52:53] neg_lo:[0,1] neg_hi:[0,1]
	v_pk_add_f32 v[52:53], v[40:41], v[44:45]
	v_pk_add_f32 v[40:41], v[40:41], v[44:45] neg_lo:[0,1] neg_hi:[0,1]
	v_pk_add_f32 v[44:45], v[26:27], v[38:39]
	v_pk_add_f32 v[26:27], v[26:27], v[38:39] neg_lo:[0,1] neg_hi:[0,1]
	v_xor_b32_e32 v39, 0x80000000, v26
	v_mov_b32_e32 v38, v27
	v_pk_add_f32 v[26:27], v[52:53], v[44:45]
	v_pk_add_f32 v[44:45], v[52:53], v[44:45] neg_lo:[0,1] neg_hi:[0,1]
	v_pk_add_f32 v[52:53], v[40:41], v[38:39]
	v_pk_add_f32 v[38:39], v[40:41], v[38:39] neg_lo:[0,1] neg_hi:[0,1]
	v_pk_add_f32 v[40:41], v[18:19], v[42:43]
	v_pk_add_f32 v[18:19], v[18:19], v[42:43] neg_lo:[0,1] neg_hi:[0,1]
	v_pk_add_f32 v[42:43], v[20:21], v[28:29]
	v_pk_add_f32 v[20:21], v[20:21], v[28:29] neg_lo:[0,1] neg_hi:[0,1]
	v_pk_mul_f32 v[28:29], v[50:51], v[20:21] op_sel:[0,1] op_sel_hi:[0,0] neg_lo:[1,1] neg_hi:[1,0]
	v_pk_fma_f32 v[20:21], v[50:51], v[20:21], v[28:29] op_sel_hi:[0,1,1]
	v_pk_add_f32 v[28:29], v[22:23], v[30:31]
	v_pk_add_f32 v[22:23], v[22:23], v[30:31] neg_lo:[0,1] neg_hi:[0,1]
	v_xor_b32_e32 v31, 0x80000000, v22
	v_mov_b32_e32 v30, v23
	v_pk_add_f32 v[22:23], v[24:25], v[32:33]
	v_pk_add_f32 v[24:25], v[24:25], v[32:33] neg_lo:[0,1] neg_hi:[0,1]
	v_pk_mul_f32 v[32:33], v[50:51], v[24:25] op_sel:[0,1] op_sel_hi:[0,0] neg_lo:[1,1] neg_hi:[1,0]
	v_pk_fma_f32 v[24:25], v[50:51], v[24:25], v[32:33] op_sel_hi:[0,1,1] neg_lo:[1,0,0] neg_hi:[1,0,0]
	v_pk_add_f32 v[32:33], v[40:41], v[28:29]
	v_pk_add_f32 v[28:29], v[40:41], v[28:29] neg_lo:[0,1] neg_hi:[0,1]
	v_pk_add_f32 v[40:41], v[42:43], v[22:23]
	v_pk_add_f32 v[22:23], v[42:43], v[22:23] neg_lo:[0,1] neg_hi:[0,1]
	v_xor_b32_e32 v43, 0x80000000, v22
	v_mov_b32_e32 v42, v23
	v_pk_add_f32 v[22:23], v[32:33], v[40:41]
	v_pk_add_f32 v[32:33], v[32:33], v[40:41] neg_lo:[0,1] neg_hi:[0,1]
	v_pk_add_f32 v[40:41], v[28:29], v[42:43]
	v_pk_add_f32 v[28:29], v[28:29], v[42:43] neg_lo:[0,1] neg_hi:[0,1]
	v_pk_add_f32 v[42:43], v[18:19], v[30:31]
	v_pk_add_f32 v[18:19], v[18:19], v[30:31] neg_lo:[0,1] neg_hi:[0,1]
	v_pk_add_f32 v[30:31], v[20:21], v[24:25]
	v_pk_add_f32 v[20:21], v[20:21], v[24:25] neg_lo:[0,1] neg_hi:[0,1]
	v_xor_b32_e32 v25, 0x80000000, v20
	v_mov_b32_e32 v24, v21
	v_pk_add_f32 v[20:21], v[42:43], v[30:31]
	v_pk_add_f32 v[30:31], v[42:43], v[30:31] neg_lo:[0,1] neg_hi:[0,1]
	v_pk_add_f32 v[42:43], v[18:19], v[24:25]
	v_pk_add_f32 v[18:19], v[18:19], v[24:25] neg_lo:[0,1] neg_hi:[0,1]
	v_add_u32_e32 v24, 0x2000, v14
	v_ashrrev_i32_e32 v25, 31, v24
	v_lshl_add_u64 v[24:25], v[24:25], 3, s[48:49]
	global_store_dwordx2 v[24:25], v[36:37], off
	v_add_u32_e32 v24, 0x2200, v14
	v_ashrrev_i32_e32 v25, 31, v24
	v_lshl_add_u64 v[24:25], v[24:25], 3, s[48:49]
	global_store_dwordx2 v[24:25], v[22:23], off
	v_add_u32_e32 v22, 0x2400, v14
	v_ashrrev_i32_e32 v23, 31, v22
	v_lshl_add_u64 v[22:23], v[22:23], 3, s[48:49]
	global_store_dwordx2 v[22:23], v[26:27], off
	v_add_u32_e32 v22, 0x2600, v14
	v_ashrrev_i32_e32 v23, 31, v22
	v_lshl_add_u64 v[22:23], v[22:23], 3, s[48:49]
	global_store_dwordx2 v[22:23], v[20:21], off
	v_add_u32_e32 v20, 0x2800, v14
	v_ashrrev_i32_e32 v21, 31, v20
	v_lshl_add_u64 v[20:21], v[20:21], 3, s[48:49]
	global_store_dwordx2 v[20:21], v[48:49], off
	v_add_u32_e32 v20, 0x2a00, v14
	v_ashrrev_i32_e32 v21, 31, v20
	v_lshl_add_u64 v[20:21], v[20:21], 3, s[48:49]
	global_store_dwordx2 v[20:21], v[40:41], off
	v_add_u32_e32 v20, 0x2c00, v14
	v_ashrrev_i32_e32 v21, 31, v20
	v_lshl_add_u64 v[20:21], v[20:21], 3, s[48:49]
	global_store_dwordx2 v[20:21], v[52:53], off
	v_add_u32_e32 v20, 0x2e00, v14
	v_ashrrev_i32_e32 v21, 31, v20
	v_lshl_add_u64 v[20:21], v[20:21], 3, s[48:49]
	global_store_dwordx2 v[20:21], v[42:43], off
	v_add_u32_e32 v20, 0x3000, v14
	v_ashrrev_i32_e32 v21, 31, v20
	v_lshl_add_u64 v[20:21], v[20:21], 3, s[48:49]
	global_store_dwordx2 v[20:21], v[46:47], off
	v_add_u32_e32 v20, 0x3200, v14
	v_ashrrev_i32_e32 v21, 31, v20
	v_lshl_add_u64 v[20:21], v[20:21], 3, s[48:49]
	global_store_dwordx2 v[20:21], v[32:33], off
	v_add_u32_e32 v20, 0x3400, v14
	v_ashrrev_i32_e32 v21, 31, v20
	v_lshl_add_u64 v[20:21], v[20:21], 3, s[48:49]
	global_store_dwordx2 v[20:21], v[44:45], off
	v_add_u32_e32 v20, 0x3600, v14
	v_ashrrev_i32_e32 v21, 31, v20
	v_lshl_add_u64 v[20:21], v[20:21], 3, s[48:49]
	global_store_dwordx2 v[20:21], v[30:31], off
	v_add_u32_e32 v20, 0x3800, v14
	v_ashrrev_i32_e32 v21, 31, v20
	v_lshl_add_u64 v[20:21], v[20:21], 3, s[48:49]
	global_store_dwordx2 v[20:21], v[34:35], off
	v_add_u32_e32 v20, 0x3a00, v14
	v_ashrrev_i32_e32 v21, 31, v20
	v_lshl_add_u64 v[20:21], v[20:21], 3, s[48:49]
	global_store_dwordx2 v[20:21], v[28:29], off
	v_add_u32_e32 v20, 0x3c00, v14
	v_add_u32_e32 v14, 0x3e00, v14
	v_ashrrev_i32_e32 v15, 31, v14
	v_ashrrev_i32_e32 v21, 31, v20
	v_lshl_add_u64 v[14:15], v[14:15], 3, s[48:49]
	v_lshl_add_u64 v[20:21], v[20:21], 3, s[48:49]
	global_store_dwordx2 v[14:15], v[18:19], off
	v_mov_b32_e32 v14, v1
	global_store_dwordx2 v[20:21], v[38:39], off
	s_barrier
	v_mov_b32_e32 v40, v170
	v_ashrrev_i32_e32 v15, 31, v14
	v_lshl_add_u64 v[18:19], v[14:15], 2, s[66:67]
	v_add_co_u32_e32 v28, vcc, s85, v18
	global_load_dword v20, v[18:19], off
	global_load_dword v21, v[18:19], off offset:2048
	v_addc_co_u32_e32 v29, vcc, 0, v19, vcc
	v_add_co_u32_e32 v22, vcc, s84, v18
	v_mov_b32_e32 v15, v174
	s_nop 0
	v_addc_co_u32_e32 v23, vcc, 0, v19, vcc
	v_add_co_u32_e32 v30, vcc, s61, v18
	v_mov_b32_e32 v45, v11
	s_nop 0
	v_addc_co_u32_e32 v31, vcc, 0, v19, vcc
	v_add_co_u32_e32 v32, vcc, s45, v18
	s_nop 1
	v_addc_co_u32_e32 v33, vcc, 0, v19, vcc
	v_add_co_u32_e32 v34, vcc, s88, v18
	global_load_dword v26, v[22:23], off offset:-4096
	global_load_dword v24, v[22:23], off
	global_load_dword v25, v[22:23], off offset:2048
	s_nop 0
	global_load_dword v22, v[32:33], off offset:-4096
	v_addc_co_u32_e32 v35, vcc, 0, v19, vcc
	v_add_co_u32_e32 v36, vcc, s0, v18
	s_mov_b32 s0, 0xa000
	s_nop 0
	v_addc_co_u32_e32 v37, vcc, 0, v19, vcc
	v_add_co_u32_e32 v38, vcc, s0, v18
	s_mov_b32 s0, 0x9000
	s_nop 0
	v_addc_co_u32_e32 v39, vcc, 0, v19, vcc
	global_load_dword v43, v[32:33], off offset:2048
	global_load_dword v46, v[34:35], off offset:-4096
	global_load_dword v48, v[36:37], off
	global_load_dword v49, v[36:37], off offset:2048
	global_load_dword v62, v[34:35], off
	global_load_dword v63, v[34:35], off offset:2048
	s_nop 0
	global_load_dword v34, v[38:39], off offset:-4096
	global_load_dword v64, v[36:37], off offset:-4096
	v_add_co_u32_e32 v36, vcc, s0, v18
	s_mov_b32 s0, 0xb000
	s_nop 0
	v_addc_co_u32_e32 v37, vcc, 0, v19, vcc
	global_load_dword v27, v[28:29], off offset:2048
	global_load_dword v35, v[36:37], off offset:2048
	v_add_co_u32_e32 v28, vcc, s86, v18
	global_load_dword v66, v[38:39], off
	global_load_dword v67, v[38:39], off offset:2048
	v_addc_co_u32_e32 v29, vcc, 0, v19, vcc
	v_add_co_u32_e32 v36, vcc, s0, v18
	s_mov_b32 s0, 0xc000
	s_nop 0
	v_addc_co_u32_e32 v37, vcc, 0, v19, vcc
	v_add_co_u32_e32 v38, vcc, s0, v18
	s_mov_b32 s0, 0xe000
	s_nop 0
	v_addc_co_u32_e32 v39, vcc, 0, v19, vcc
	global_load_dword v68, v[38:39], off offset:-4096
	global_load_dword v23, v[30:31], off offset:2048
	global_load_dword v69, v[36:37], off offset:2048
	v_add_co_u32_e32 v30, vcc, s90, v18
	s_waitcnt vmcnt(11)
	v_sub_f32_e32 v44, v21, v49
	v_addc_co_u32_e32 v31, vcc, 0, v19, vcc
	global_load_dword v47, v[28:29], off offset:2048
	global_load_dword v65, v[30:31], off offset:2048
	global_load_dword v42, v[32:33], off
	s_nop 0
	global_load_dword v30, v[38:39], off
	global_load_dword v31, v[38:39], off offset:2048
	v_add_co_u32_e32 v28, vcc, s0, v18
	s_mov_b32 s0, 0xd000
	s_nop 0
	v_addc_co_u32_e32 v29, vcc, 0, v19, vcc
	global_load_dword v32, v[28:29], off offset:-4096
	v_add_co_u32_e32 v36, vcc, s0, v18
	s_mov_b32 s0, 0xf000
	s_nop 0
	v_addc_co_u32_e32 v37, vcc, 0, v19, vcc
	global_load_dword v33, v[36:37], off offset:2048
	global_load_dword v38, v[28:29], off
	global_load_dword v39, v[28:29], off offset:2048
	v_add_co_u32_e32 v18, vcc, s0, v18
	v_mov_b32_e32 v36, v166
	s_nop 0
	v_addc_co_u32_e32 v19, vcc, 0, v19, vcc
	global_load_dword v70, v[18:19], off
	global_load_dword v71, v[18:19], off offset:2048
	v_mov_b32_e32 v28, v168
	v_mov_b32_e32 v13, v44
	s_nop 0
	v_mov_b32_e32 v10, v172
	v_pk_mul_f32 v[50:51], v[12:13], v[78:79] op_sel_hi:[1,0] neg_lo:[0,1] neg_hi:[0,1]
	s_waitcnt vmcnt(6)
	v_sub_f32_e32 v82, v43, v31
	v_pk_fma_f32 v[44:45], v[44:45], v[72:73], v[50:51] op_sel_hi:[1,0,1]
	v_sub_f32_e32 v50, v26, v34
	v_mov_b32_e32 v13, v50
	v_mov_b32_e32 v51, v11
	v_pk_mul_f32 v[52:53], v[12:13], v[40:41] op_sel_hi:[1,0] neg_lo:[0,1] neg_hi:[0,1]
	v_pk_mul_f32 v[84:85], v[82:83], v[78:79] op_sel_hi:[1,0] neg_lo:[0,1] neg_hi:[0,1]
	v_pk_fma_f32 v[50:51], v[50:51], v[36:37], v[52:53] op_sel_hi:[1,0,1]
	v_sub_f32_e32 v52, v27, v35
	v_mov_b32_e32 v13, v52
	v_mov_b32_e32 v53, v11
	v_pk_mul_f32 v[54:55], v[12:13], v[76:77] op_sel_hi:[1,0] neg_lo:[0,1] neg_hi:[0,1]
	v_sub_f32_e32 v10, v20, v48
	v_pk_fma_f32 v[54:55], v[52:53], v[74:75], v[54:55] op_sel_hi:[1,0,1]
	v_sub_f32_e32 v52, v24, v66
	v_mov_b32_e32 v13, v52
	v_pk_mul_f32 v[56:57], v[12:13], v[28:29] op_sel_hi:[1,0] neg_lo:[0,1] neg_hi:[0,1]
	v_pk_add_f32 v[20:21], v[20:21], v[48:49]
	v_pk_fma_f32 v[56:57], v[52:53], v[28:29], v[56:57] op_sel_hi:[1,0,1]
	v_sub_f32_e32 v52, v25, v67
	v_pk_mul_f32 v[58:59], v[52:53], v[76:77] op_sel_hi:[1,0]
	v_mov_b32_e32 v13, v52
	v_sub_f32_e32 v52, v22, v68
	v_pk_fma_f32 v[60:61], v[12:13], v[74:75], v[58:59] op_sel_hi:[1,0,1] neg_lo:[0,1,0] neg_hi:[0,1,0]
	v_pk_mul_f32 v[58:59], v[52:53], v[40:41] op_sel_hi:[1,0]
	v_mov_b32_e32 v13, v52
	v_sub_f32_e32 v52, v23, v69
	v_pk_fma_f32 v[58:59], v[12:13], v[36:37], v[58:59] op_sel_hi:[1,0,1] neg_lo:[0,1,0] neg_hi:[0,1,0]
	v_pk_mul_f32 v[80:81], v[52:53], v[78:79] op_sel_hi:[1,0]
	v_mov_b32_e32 v13, v52
	v_pk_fma_f32 v[52:53], v[12:13], v[72:73], v[80:81] op_sel_hi:[1,0,1] neg_lo:[0,1,0] neg_hi:[0,1,0]
	v_sub_f32_e32 v13, v42, v30
	v_xor_b32_e32 v81, 0x80000000, v13
	v_mov_b32_e32 v13, v82
	v_pk_fma_f32 v[82:83], v[12:13], v[72:73], v[84:85] op_sel_hi:[1,0,1] neg_lo:[0,1,0] neg_hi:[0,1,0]
	s_waitcnt vmcnt(5)
	v_sub_f32_e32 v84, v46, v32
	v_mov_b32_e32 v85, v11
	v_pk_mul_f32 v[86:87], v[84:85], v[40:41] op_sel_hi:[1,0] neg_lo:[0,1] neg_hi:[0,1]
	v_mov_b32_e32 v13, v84
	v_pk_fma_f32 v[84:85], v[12:13], v[36:37], v[86:87] op_sel_hi:[1,0,1] neg_lo:[0,1,0] neg_hi:[0,1,0]
	s_waitcnt vmcnt(4)
	v_sub_f32_e32 v86, v47, v33
	v_mov_b32_e32 v87, v11
	v_pk_mul_f32 v[88:89], v[86:87], v[76:77] op_sel_hi:[1,0] neg_lo:[0,1] neg_hi:[0,1]
	v_mov_b32_e32 v13, v86
	v_pk_fma_f32 v[86:87], v[12:13], v[74:75], v[88:89] op_sel_hi:[1,0,1] neg_lo:[0,1,0] neg_hi:[0,1,0]
	s_waitcnt vmcnt(3)
	v_sub_f32_e32 v88, v62, v38
	v_mov_b32_e32 v13, v88
	v_mov_b32_e32 v89, v11
	v_pk_mul_f32 v[90:91], v[12:13], v[28:29] op_sel_hi:[1,0] neg_lo:[0,1] neg_hi:[0,1]
	v_pk_add_f32 v[30:31], v[42:43], v[30:31]
	v_pk_fma_f32 v[88:89], v[88:89], v[28:29], v[90:91] op_sel_hi:[1,0,1] neg_lo:[0,1,0] neg_hi:[0,1,0]
	s_waitcnt vmcnt(2)
	v_sub_f32_e32 v90, v63, v39
	v_mov_b32_e32 v13, v90
	v_mov_b32_e32 v91, v11
	v_pk_mul_f32 v[76:77], v[12:13], v[76:77] op_sel_hi:[1,0] neg_lo:[0,1] neg_hi:[0,1]
	v_pk_add_f32 v[42:43], v[20:21], v[30:31] neg_lo:[0,1] neg_hi:[0,1]
	v_pk_fma_f32 v[74:75], v[90:91], v[74:75], v[76:77] op_sel_hi:[1,0,1] neg_lo:[0,1,0] neg_hi:[0,1,0]
	s_waitcnt vmcnt(1)
	v_sub_f32_e32 v76, v64, v70
	v_mov_b32_e32 v13, v76
	v_mov_b32_e32 v77, v11
	v_pk_mul_f32 v[90:91], v[12:13], v[40:41] op_sel_hi:[1,0] neg_lo:[0,1] neg_hi:[0,1]
	v_pk_add_f32 v[26:27], v[26:27], v[34:35]
	v_pk_fma_f32 v[76:77], v[76:77], v[36:37], v[90:91] op_sel_hi:[1,0,1] neg_lo:[0,1,0] neg_hi:[0,1,0]
	s_waitcnt vmcnt(0)
	v_sub_f32_e32 v90, v65, v71
	v_mov_b32_e32 v13, v90
	v_pk_mul_f32 v[78:79], v[12:13], v[78:79] op_sel_hi:[1,0] neg_lo:[0,1] neg_hi:[0,1]
	v_mov_b32_e32 v13, v43
	v_pk_add_f32 v[32:33], v[46:47], v[32:33]
	v_mov_b32_e32 v46, v42
	v_pk_add_f32 v[20:21], v[20:21], v[30:31]
	v_mov_b32_e32 v30, v43
	v_mov_b32_e32 v31, v11
	v_pk_mul_f32 v[42:43], v[12:13], v[40:41] op_sel_hi:[1,0] neg_lo:[0,1] neg_hi:[0,1]
	v_pk_add_f32 v[34:35], v[62:63], v[38:39]
	v_pk_fma_f32 v[62:63], v[30:31], v[36:37], v[42:43] op_sel_hi:[1,0,1]
	v_pk_add_f32 v[30:31], v[26:27], v[32:33] neg_lo:[0,1] neg_hi:[0,1]
	v_pk_add_f32 v[24:25], v[24:25], v[66:67]
	v_mov_b32_e32 v13, v30
	v_mov_b32_e32 v42, v30
	v_pk_mul_f32 v[48:49], v[12:13], v[28:29] op_sel_hi:[1,0] neg_lo:[0,1] neg_hi:[0,1]
	v_pk_add_f32 v[26:27], v[26:27], v[32:33]
	v_mov_b32_e32 v32, v31
	v_mov_b32_e32 v33, v11
	v_mov_b32_e32 v13, v31
	v_pk_add_f32 v[30:31], v[24:25], v[34:35] neg_lo:[0,1] neg_hi:[0,1]
	v_pk_add_f32 v[22:23], v[22:23], v[68:69]
	v_pk_add_f32 v[38:39], v[64:65], v[70:71]
	v_pk_mul_f32 v[32:33], v[32:33], v[40:41] op_sel_hi:[1,0]
	v_pk_add_f32 v[24:25], v[24:25], v[34:35]
	v_mov_b32_e32 v34, v31
	v_mov_b32_e32 v35, v11
	v_pk_fma_f32 v[32:33], v[12:13], v[36:37], v[32:33] op_sel_hi:[1,0,1] neg_lo:[0,1,0] neg_hi:[0,1,0]
	v_xor_b32_e32 v67, 0x80000000, v30
	v_pk_mul_f32 v[34:35], v[34:35], v[40:41] op_sel_hi:[1,0] neg_lo:[0,1] neg_hi:[0,1]
	v_mov_b32_e32 v13, v31
	v_pk_add_f32 v[30:31], v[22:23], v[38:39] neg_lo:[0,1] neg_hi:[0,1]
	v_mov_b32_e32 v43, v11
	v_pk_fma_f32 v[68:69], v[12:13], v[36:37], v[34:35] op_sel_hi:[1,0,1] neg_lo:[0,1,0] neg_hi:[0,1,0]
	v_mov_b32_e32 v13, v30
	v_pk_fma_f32 v[64:65], v[42:43], v[28:29], v[48:49] op_sel_hi:[1,0,1]
	v_mov_b32_e32 v34, v30
	v_mov_b32_e32 v35, v11
	v_pk_mul_f32 v[42:43], v[12:13], v[28:29] op_sel_hi:[1,0] neg_lo:[0,1] neg_hi:[0,1]
	v_mov_b32_e32 v13, v31
	v_pk_fma_f32 v[70:71], v[34:35], v[28:29], v[42:43] op_sel_hi:[1,0,1] neg_lo:[0,1,0] neg_hi:[0,1,0]
	v_mov_b32_e32 v34, v31
	v_pk_mul_f32 v[30:31], v[12:13], v[40:41] op_sel_hi:[1,0] neg_lo:[0,1] neg_hi:[0,1]
	v_pk_add_f32 v[22:23], v[22:23], v[38:39]
	v_pk_fma_f32 v[38:39], v[34:35], v[36:37], v[30:31] op_sel_hi:[1,0,1] neg_lo:[0,1,0] neg_hi:[0,1,0]
	v_pk_add_f32 v[30:31], v[20:21], v[24:25] neg_lo:[0,1] neg_hi:[0,1]
	v_pk_add_f32 v[20:21], v[20:21], v[24:25]
	v_mov_b32_e32 v13, v31
	v_mov_b32_e32 v42, v30
	v_mov_b32_e32 v24, v31
	v_mov_b32_e32 v25, v11
	v_pk_mul_f32 v[30:31], v[12:13], v[28:29] op_sel_hi:[1,0] neg_lo:[0,1] neg_hi:[0,1]
	v_mov_b32_e32 v91, v11
	v_pk_fma_f32 v[30:31], v[24:25], v[28:29], v[30:31] op_sel_hi:[1,0,1]
	v_pk_add_f32 v[24:25], v[26:27], v[22:23] neg_lo:[0,1] neg_hi:[0,1]
	v_pk_fma_f32 v[72:73], v[90:91], v[72:73], v[78:79] op_sel_hi:[1,0,1] neg_lo:[0,1,0] neg_hi:[0,1,0]
	v_mov_b32_e32 v13, v25
	v_xor_b32_e32 v79, 0x80000000, v24
	v_pk_add_f32 v[22:23], v[26:27], v[22:23]
	v_mov_b32_e32 v26, v25
	v_mov_b32_e32 v27, v11
	v_pk_mul_f32 v[24:25], v[12:13], v[28:29] op_sel_hi:[1,0] neg_lo:[0,1] neg_hi:[0,1]
	v_pk_add_f32 v[34:35], v[20:21], v[22:23]
	v_pk_fma_f32 v[26:27], v[26:27], v[28:29], v[24:25] op_sel_hi:[1,0,1] neg_lo:[0,1,0] neg_hi:[0,1,0]
	v_pk_add_f32 v[24:25], v[20:21], v[22:23] neg_lo:[0,1] neg_hi:[0,1]
	v_mov_b32_e32 v43, v11
	v_pk_add_f32 v[20:21], v[24:25], 0 neg_lo:[1,1] neg_hi:[1,1]
	v_mov_b32_e32 v78, v11
	v_mov_b32_e32 v90, v24
	v_mov_b32_e32 v20, v11
	v_pk_add_f32 v[48:49], v[90:91], v[20:21]
	v_pk_add_f32 v[24:25], v[90:91], v[20:21] neg_lo:[0,1] neg_hi:[0,1]
	v_pk_add_f32 v[20:21], v[42:43], v[78:79]
	v_pk_add_f32 v[22:23], v[42:43], v[78:79] neg_lo:[0,1] neg_hi:[0,1]
	v_pk_add_f32 v[42:43], v[30:31], v[26:27]
	v_pk_add_f32 v[26:27], v[30:31], v[26:27] neg_lo:[0,1] neg_hi:[0,1]
	v_mov_b32_e32 v47, v11
	v_mov_b32_e32 v66, v11
	v_xor_b32_e32 v79, 0x80000000, v26
	v_mov_b32_e32 v78, v27
	v_pk_add_f32 v[26:27], v[62:63], v[68:69]
	v_pk_add_f32 v[62:63], v[62:63], v[68:69] neg_lo:[0,1] neg_hi:[0,1]
	v_pk_add_f32 v[90:91], v[20:21], v[42:43]
	v_pk_add_f32 v[30:31], v[20:21], v[42:43] neg_lo:[0,1] neg_hi:[0,1]
	v_pk_add_f32 v[42:43], v[22:23], v[78:79]
	v_pk_add_f32 v[20:21], v[22:23], v[78:79] neg_lo:[0,1] neg_hi:[0,1]
	v_pk_add_f32 v[22:23], v[46:47], v[66:67]
	v_pk_add_f32 v[46:47], v[46:47], v[66:67] neg_lo:[0,1] neg_hi:[0,1]
	v_pk_mul_f32 v[66:67], v[28:29], v[62:63] op_sel:[0,1] op_sel_hi:[0,0] neg_lo:[1,1] neg_hi:[1,0]
	v_pk_fma_f32 v[66:67], v[28:29], v[62:63], v[66:67] op_sel_hi:[0,1,1]
	v_pk_add_f32 v[62:63], v[64:65], v[70:71]
	v_pk_add_f32 v[64:65], v[64:65], v[70:71] neg_lo:[0,1] neg_hi:[0,1]
	v_mov_b32_e32 v80, v11
	v_xor_b32_e32 v69, 0x80000000, v64
	v_mov_b32_e32 v68, v65
	v_pk_add_f32 v[64:65], v[32:33], v[38:39]
	v_pk_add_f32 v[32:33], v[32:33], v[38:39] neg_lo:[0,1] neg_hi:[0,1]
	v_pk_add_f32 v[78:79], v[44:45], v[82:83]
	v_pk_mul_f32 v[38:39], v[28:29], v[32:33] op_sel:[0,1] op_sel_hi:[0,0] neg_lo:[1,1] neg_hi:[1,0]
	v_pk_fma_f32 v[32:33], v[28:29], v[32:33], v[38:39] op_sel_hi:[0,1,1] neg_lo:[1,0,0] neg_hi:[1,0,0]
	v_pk_add_f32 v[38:39], v[22:23], v[62:63]
	v_pk_add_f32 v[22:23], v[22:23], v[62:63] neg_lo:[0,1] neg_hi:[0,1]
	v_pk_add_f32 v[62:63], v[26:27], v[64:65]
	v_pk_add_f32 v[26:27], v[26:27], v[64:65] neg_lo:[0,1] neg_hi:[0,1]
	v_pk_add_f32 v[70:71], v[38:39], v[62:63]
	v_pk_add_f32 v[38:39], v[38:39], v[62:63] neg_lo:[0,1] neg_hi:[0,1]
	v_pk_add_f32 v[62:63], v[22:23], v[26:27] op_sel:[0,1] op_sel_hi:[1,0] neg_hi:[0,1]
	v_pk_add_f32 v[26:27], v[22:23], v[26:27] op_sel:[0,1] op_sel_hi:[1,0] neg_lo:[0,1]
	v_pk_add_f32 v[22:23], v[46:47], v[68:69]
	v_pk_add_f32 v[64:65], v[46:47], v[68:69] neg_lo:[0,1] neg_hi:[0,1]
	v_pk_add_f32 v[46:47], v[66:67], v[32:33]
	v_pk_add_f32 v[32:33], v[66:67], v[32:33] neg_lo:[0,1] neg_hi:[0,1]
	v_pk_add_f32 v[44:45], v[44:45], v[82:83] neg_lo:[0,1] neg_hi:[0,1]
	v_xor_b32_e32 v67, 0x80000000, v32
	v_mov_b32_e32 v66, v33
	v_pk_add_f32 v[68:69], v[22:23], v[46:47]
	v_pk_add_f32 v[32:33], v[22:23], v[46:47] neg_lo:[0,1] neg_hi:[0,1]
	v_pk_add_f32 v[46:47], v[64:65], v[66:67]
	v_pk_add_f32 v[22:23], v[64:65], v[66:67] neg_lo:[0,1] neg_hi:[0,1]
	v_pk_add_f32 v[64:65], v[10:11], v[80:81]
	v_pk_add_f32 v[66:67], v[10:11], v[80:81] neg_lo:[0,1] neg_hi:[0,1]
	v_pk_mul_f32 v[80:81], v[40:41], v[44:45] op_sel:[0,1] op_sel_hi:[0,0] neg_lo:[1,1] neg_hi:[1,0]
	v_pk_fma_f32 v[44:45], v[36:37], v[44:45], v[80:81] op_sel_hi:[0,1,1]
	v_pk_add_f32 v[80:81], v[50:51], v[84:85]
	v_pk_add_f32 v[50:51], v[50:51], v[84:85] neg_lo:[0,1] neg_hi:[0,1]
	v_add_f32_e32 v10, v34, v35
	v_pk_mul_f32 v[82:83], v[28:29], v[50:51] op_sel:[0,1] op_sel_hi:[0,0] neg_lo:[1,1] neg_hi:[1,0]
	v_pk_fma_f32 v[82:83], v[28:29], v[50:51], v[82:83] op_sel_hi:[0,1,1]
	v_pk_add_f32 v[50:51], v[54:55], v[86:87]
	v_pk_add_f32 v[54:55], v[54:55], v[86:87] neg_lo:[0,1] neg_hi:[0,1]
	v_pk_fma_f32 v[16:17], v[10:11], s[42:43], v[16:17] op_sel_hi:[0,1,1]
	v_pk_mul_f32 v[84:85], v[36:37], v[54:55] op_sel:[0,1] op_sel_hi:[0,0] neg_lo:[1,1] neg_hi:[1,0]
	v_pk_fma_f32 v[84:85], v[40:41], v[54:55], v[84:85] op_sel_hi:[0,1,1]
	v_pk_add_f32 v[54:55], v[56:57], v[88:89]
	v_pk_add_f32 v[56:57], v[56:57], v[88:89] neg_lo:[0,1] neg_hi:[0,1]
	v_lshl_add_u32 v13, v15, 3, 0
	v_xor_b32_e32 v87, 0x80000000, v56
	v_mov_b32_e32 v86, v57
	v_pk_add_f32 v[56:57], v[60:61], v[74:75]
	v_pk_add_f32 v[60:61], v[60:61], v[74:75] neg_lo:[0,1] neg_hi:[0,1]
	ds_write_b64 v13, v[16:17]
	v_pk_mul_f32 v[74:75], v[36:37], v[60:61] op_sel:[0,1] op_sel_hi:[0,0] neg_lo:[1,1] neg_hi:[1,0]
	v_pk_fma_f32 v[60:61], v[40:41], v[60:61], v[74:75] op_sel_hi:[0,1,1] neg_lo:[1,0,0] neg_hi:[1,0,0]
	v_pk_add_f32 v[74:75], v[58:59], v[76:77]
	v_pk_add_f32 v[58:59], v[58:59], v[76:77] neg_lo:[0,1] neg_hi:[0,1]
	v_pk_fma_f32 v[16:17], v[180:181], s[92:93], v[180:181] op_sel:[1,0,0] op_sel_hi:[0,1,1]
	v_pk_mul_f32 v[76:77], v[28:29], v[58:59] op_sel:[0,1] op_sel_hi:[0,0] neg_lo:[1,1] neg_hi:[1,0]
	v_pk_fma_f32 v[58:59], v[28:29], v[58:59], v[76:77] op_sel_hi:[0,1,1] neg_lo:[1,0,0] neg_hi:[1,0,0]
	v_pk_add_f32 v[76:77], v[52:53], v[72:73]
	v_pk_add_f32 v[52:53], v[52:53], v[72:73] neg_lo:[0,1] neg_hi:[0,1]
	v_pk_mul_f32 v[40:41], v[40:41], v[52:53] op_sel:[0,1] op_sel_hi:[0,0] neg_lo:[1,1] neg_hi:[1,0]
	v_pk_fma_f32 v[52:53], v[36:37], v[52:53], v[40:41] op_sel_hi:[0,1,1] neg_lo:[1,0,0] neg_hi:[1,0,0]
	v_pk_add_f32 v[36:37], v[64:65], v[54:55]
	v_pk_add_f32 v[64:65], v[64:65], v[54:55] neg_lo:[0,1] neg_hi:[0,1]
	v_pk_add_f32 v[54:55], v[78:79], v[56:57] neg_lo:[0,1] neg_hi:[0,1]
	v_pk_add_f32 v[40:41], v[56:57], v[78:79]
	v_pk_mul_f32 v[56:57], v[28:29], v[54:55] op_sel:[0,1] op_sel_hi:[0,0] neg_lo:[1,1] neg_hi:[1,0]
	v_pk_add_f32 v[72:73], v[80:81], v[74:75] neg_lo:[0,1] neg_hi:[0,1]
	v_pk_fma_f32 v[56:57], v[28:29], v[54:55], v[56:57] op_sel_hi:[0,1,1]
	v_pk_add_f32 v[54:55], v[80:81], v[74:75]
	v_xor_b32_e32 v75, 0x80000000, v72
	v_mov_b32_e32 v74, v73
	v_pk_add_f32 v[72:73], v[50:51], v[76:77]
	v_pk_add_f32 v[50:51], v[50:51], v[76:77] neg_lo:[0,1] neg_hi:[0,1]
	v_pk_mul_f32 v[76:77], v[28:29], v[50:51] op_sel:[0,1] op_sel_hi:[0,0] neg_lo:[1,1] neg_hi:[1,0]
	v_pk_fma_f32 v[50:51], v[28:29], v[50:51], v[76:77] op_sel_hi:[0,1,1] neg_lo:[1,0,0] neg_hi:[1,0,0]
	v_pk_add_f32 v[76:77], v[36:37], v[54:55]
	v_pk_add_f32 v[36:37], v[36:37], v[54:55] neg_lo:[0,1] neg_hi:[0,1]
	v_pk_add_f32 v[54:55], v[40:41], v[72:73]
	v_pk_add_f32 v[40:41], v[40:41], v[72:73] neg_lo:[0,1] neg_hi:[0,1]
	v_pk_add_f32 v[78:79], v[76:77], v[54:55]
	v_pk_add_f32 v[54:55], v[76:77], v[54:55] neg_lo:[0,1] neg_hi:[0,1]
	v_pk_add_f32 v[76:77], v[36:37], v[40:41] op_sel:[0,1] op_sel_hi:[1,0] neg_hi:[0,1]
	v_pk_add_f32 v[40:41], v[36:37], v[40:41] op_sel:[0,1] op_sel_hi:[1,0] neg_lo:[0,1]
	v_pk_add_f32 v[72:73], v[56:57], v[50:51]
	v_pk_add_f32 v[50:51], v[56:57], v[50:51] neg_lo:[0,1] neg_hi:[0,1]
	v_pk_add_f32 v[36:37], v[64:65], v[74:75]
	v_pk_add_f32 v[64:65], v[64:65], v[74:75] neg_lo:[0,1] neg_hi:[0,1]
	v_xor_b32_e32 v57, 0x80000000, v50
	v_mov_b32_e32 v56, v51
	v_pk_add_f32 v[74:75], v[36:37], v[72:73]
	v_pk_add_f32 v[50:51], v[36:37], v[72:73] neg_lo:[0,1] neg_hi:[0,1]
	v_pk_add_f32 v[72:73], v[64:65], v[56:57]
	v_pk_add_f32 v[36:37], v[64:65], v[56:57] neg_lo:[0,1] neg_hi:[0,1]
	v_pk_add_f32 v[56:57], v[66:67], v[86:87]
	v_pk_add_f32 v[64:65], v[66:67], v[86:87] neg_lo:[0,1] neg_hi:[0,1]
	v_pk_add_f32 v[66:67], v[60:61], v[44:45]
	v_pk_add_f32 v[44:45], v[44:45], v[60:61] neg_lo:[0,1] neg_hi:[0,1]
	v_pk_mul_f32 v[60:61], v[28:29], v[44:45] op_sel:[0,1] op_sel_hi:[0,0] neg_lo:[1,1] neg_hi:[1,0]
	v_pk_fma_f32 v[60:61], v[28:29], v[44:45], v[60:61] op_sel_hi:[0,1,1]
	v_pk_add_f32 v[44:45], v[82:83], v[58:59]
	v_pk_add_f32 v[58:59], v[82:83], v[58:59] neg_lo:[0,1] neg_hi:[0,1]
	v_xor_b32_e32 v81, 0x80000000, v58
	v_mov_b32_e32 v80, v59
	v_pk_add_f32 v[58:59], v[84:85], v[52:53]
	v_pk_add_f32 v[52:53], v[84:85], v[52:53] neg_lo:[0,1] neg_hi:[0,1]
	v_pk_mul_f32 v[82:83], v[28:29], v[52:53] op_sel:[0,1] op_sel_hi:[0,0] neg_lo:[1,1] neg_hi:[1,0]
	v_pk_fma_f32 v[28:29], v[28:29], v[52:53], v[82:83] op_sel_hi:[0,1,1] neg_lo:[1,0,0] neg_hi:[1,0,0]
	v_pk_add_f32 v[52:53], v[56:57], v[44:45]
	v_pk_add_f32 v[44:45], v[56:57], v[44:45] neg_lo:[0,1] neg_hi:[0,1]
	v_pk_add_f32 v[56:57], v[66:67], v[58:59]
	v_pk_add_f32 v[58:59], v[66:67], v[58:59] neg_lo:[0,1] neg_hi:[0,1]
	v_pk_add_f32 v[82:83], v[44:45], v[58:59] op_sel:[0,1] op_sel_hi:[1,0] neg_hi:[0,1]
	v_pk_add_f32 v[44:45], v[44:45], v[58:59] op_sel:[0,1] op_sel_hi:[1,0] neg_lo:[0,1]
	v_pk_add_f32 v[66:67], v[60:61], v[28:29]
	v_pk_add_f32 v[28:29], v[60:61], v[28:29] neg_lo:[0,1] neg_hi:[0,1]
	v_pk_add_f32 v[58:59], v[52:53], v[56:57]
	v_pk_add_f32 v[56:57], v[52:53], v[56:57] neg_lo:[0,1] neg_hi:[0,1]
	v_pk_add_f32 v[52:53], v[64:65], v[80:81]
	v_pk_add_f32 v[64:65], v[64:65], v[80:81] neg_lo:[0,1] neg_hi:[0,1]
	v_pk_add_f32 v[80:81], v[52:53], v[66:67]
	v_pk_add_f32 v[52:53], v[52:53], v[66:67] neg_lo:[0,1] neg_hi:[0,1]
	v_pk_add_f32 v[66:67], v[64:65], v[28:29] op_sel:[0,1] op_sel_hi:[1,0] neg_hi:[0,1]
	v_pk_add_f32 v[28:29], v[64:65], v[28:29] op_sel:[0,1] op_sel_hi:[1,0] neg_lo:[0,1]
	v_pk_mul_f32 v[60:61], v[16:17], v[78:79] op_sel:[1,1] op_sel_hi:[0,1] neg_lo:[0,1]
	v_pk_fma_f32 v[60:61], v[16:17], v[78:79], v[60:61] op_sel_hi:[1,0,1]
	ds_write_b64 v13, v[60:61] offset:4224
	v_pk_mul_f32 v[60:61], v[180:181], v[16:17] op_sel:[1,1] op_sel_hi:[0,1] neg_lo:[0,1]
	v_pk_fma_f32 v[16:17], v[180:181], v[16:17], v[60:61] op_sel_hi:[1,0,1]
	v_pk_mul_f32 v[60:61], v[16:17], v[70:71] op_sel:[1,1] op_sel_hi:[0,1] neg_lo:[0,1]
	v_pk_fma_f32 v[60:61], v[16:17], v[70:71], v[60:61] op_sel_hi:[1,0,1]
	ds_write_b64 v13, v[60:61] offset:8448
	v_pk_mul_f32 v[60:61], v[180:181], v[16:17] op_sel:[1,1] op_sel_hi:[0,1] neg_lo:[0,1]
	v_pk_fma_f32 v[16:17], v[180:181], v[16:17], v[60:61] op_sel_hi:[1,0,1]
	v_pk_mul_f32 v[60:61], v[16:17], v[58:59] op_sel:[1,1] op_sel_hi:[0,1] neg_lo:[0,1]
	v_pk_fma_f32 v[58:59], v[16:17], v[58:59], v[60:61] op_sel_hi:[1,0,1]
	ds_write_b64 v13, v[58:59] offset:12672
	v_pk_mul_f32 v[58:59], v[180:181], v[16:17] op_sel:[1,1] op_sel_hi:[0,1] neg_lo:[0,1]
	v_pk_fma_f32 v[16:17], v[180:181], v[16:17], v[58:59] op_sel_hi:[1,0,1]
	v_pk_mul_f32 v[58:59], v[90:91], v[16:17] op_sel:[1,1] op_sel_hi:[1,0] neg_lo:[1,0]
	v_pk_fma_f32 v[58:59], v[90:91], v[16:17], v[58:59] op_sel_hi:[0,1,1]
	ds_write_b64 v13, v[58:59] offset:16896
	v_pk_mul_f32 v[58:59], v[180:181], v[16:17] op_sel:[1,1] op_sel_hi:[0,1] neg_lo:[0,1]
	v_pk_fma_f32 v[16:17], v[180:181], v[16:17], v[58:59] op_sel_hi:[1,0,1]
	v_pk_mul_f32 v[58:59], v[16:17], v[74:75] op_sel:[1,1] op_sel_hi:[0,1] neg_lo:[0,1]
	v_pk_fma_f32 v[58:59], v[16:17], v[74:75], v[58:59] op_sel_hi:[1,0,1]
	ds_write_b64 v13, v[58:59] offset:21120
	v_pk_mul_f32 v[58:59], v[180:181], v[16:17] op_sel:[1,1] op_sel_hi:[0,1] neg_lo:[0,1]
	v_pk_fma_f32 v[16:17], v[180:181], v[16:17], v[58:59] op_sel_hi:[1,0,1]
	v_pk_mul_f32 v[58:59], v[68:69], v[16:17] op_sel:[1,1] op_sel_hi:[1,0] neg_lo:[1,0]
	v_pk_fma_f32 v[58:59], v[68:69], v[16:17], v[58:59] op_sel_hi:[0,1,1]
	ds_write_b64 v13, v[58:59] offset:25344
	v_pk_mul_f32 v[58:59], v[180:181], v[16:17] op_sel:[1,1] op_sel_hi:[0,1] neg_lo:[0,1]
	v_pk_fma_f32 v[16:17], v[180:181], v[16:17], v[58:59] op_sel_hi:[1,0,1]
	v_pk_mul_f32 v[58:59], v[80:81], v[16:17] op_sel:[1,1] op_sel_hi:[1,0] neg_lo:[1,0]
	v_pk_fma_f32 v[58:59], v[80:81], v[16:17], v[58:59] op_sel_hi:[0,1,1]
	ds_write_b64 v13, v[58:59] offset:29568
	v_pk_mul_f32 v[58:59], v[180:181], v[16:17] op_sel:[1,1] op_sel_hi:[0,1] neg_lo:[0,1]
	v_pk_fma_f32 v[16:17], v[180:181], v[16:17], v[58:59] op_sel_hi:[1,0,1]
	v_pk_mul_f32 v[58:59], v[48:49], v[16:17] op_sel:[1,1] op_sel_hi:[1,0] neg_lo:[1,0]
	v_pk_fma_f32 v[48:49], v[48:49], v[16:17], v[58:59] op_sel_hi:[0,1,1]
	ds_write_b64 v13, v[48:49] offset:33792
	v_pk_mul_f32 v[48:49], v[180:181], v[16:17] op_sel:[1,1] op_sel_hi:[0,1] neg_lo:[0,1]
	v_pk_fma_f32 v[16:17], v[180:181], v[16:17], v[48:49] op_sel_hi:[1,0,1]
	v_pk_mul_f32 v[48:49], v[76:77], v[16:17] op_sel:[1,1] op_sel_hi:[1,0] neg_lo:[1,0]
	v_pk_fma_f32 v[48:49], v[76:77], v[16:17], v[48:49] op_sel_hi:[0,1,1]
	ds_write_b64 v13, v[48:49] offset:38016
	v_pk_mul_f32 v[48:49], v[180:181], v[16:17] op_sel:[1,1] op_sel_hi:[0,1] neg_lo:[0,1]
	v_pk_fma_f32 v[16:17], v[180:181], v[16:17], v[48:49] op_sel_hi:[1,0,1]
	v_pk_mul_f32 v[48:49], v[62:63], v[16:17] op_sel:[1,1] op_sel_hi:[1,0] neg_lo:[1,0]
	v_pk_fma_f32 v[48:49], v[62:63], v[16:17], v[48:49] op_sel_hi:[0,1,1]
	ds_write_b64 v13, v[48:49] offset:42240
	v_pk_mul_f32 v[48:49], v[180:181], v[16:17] op_sel:[1,1] op_sel_hi:[0,1] neg_lo:[0,1]
	v_pk_fma_f32 v[16:17], v[180:181], v[16:17], v[48:49] op_sel_hi:[1,0,1]
	v_pk_mul_f32 v[48:49], v[82:83], v[16:17] op_sel:[1,1] op_sel_hi:[1,0] neg_lo:[1,0]
	v_pk_fma_f32 v[48:49], v[82:83], v[16:17], v[48:49] op_sel_hi:[0,1,1]
	ds_write_b64 v13, v[48:49] offset:46464
	v_pk_mul_f32 v[48:49], v[180:181], v[16:17] op_sel:[1,1] op_sel_hi:[0,1] neg_lo:[0,1]
	v_pk_fma_f32 v[16:17], v[180:181], v[16:17], v[48:49] op_sel_hi:[1,0,1]
	v_pk_mul_f32 v[48:49], v[42:43], v[16:17] op_sel:[1,1] op_sel_hi:[1,0] neg_lo:[1,0]
	v_pk_fma_f32 v[42:43], v[42:43], v[16:17], v[48:49] op_sel_hi:[0,1,1]
	ds_write_b64 v13, v[42:43] offset:50688
	v_pk_mul_f32 v[42:43], v[180:181], v[16:17] op_sel:[1,1] op_sel_hi:[0,1] neg_lo:[0,1]
	v_pk_fma_f32 v[16:17], v[180:181], v[16:17], v[42:43] op_sel_hi:[1,0,1]
	v_pk_mul_f32 v[42:43], v[72:73], v[16:17] op_sel:[1,1] op_sel_hi:[1,0] neg_lo:[1,0]
	v_pk_fma_f32 v[42:43], v[72:73], v[16:17], v[42:43] op_sel_hi:[0,1,1]
	ds_write_b64 v13, v[42:43] offset:54912
	v_pk_mul_f32 v[42:43], v[180:181], v[16:17] op_sel:[1,1] op_sel_hi:[0,1] neg_lo:[0,1]
	v_pk_fma_f32 v[16:17], v[180:181], v[16:17], v[42:43] op_sel_hi:[1,0,1]
	v_pk_mul_f32 v[42:43], v[46:47], v[16:17] op_sel:[1,1] op_sel_hi:[1,0] neg_lo:[1,0]
	v_pk_fma_f32 v[42:43], v[46:47], v[16:17], v[42:43] op_sel_hi:[0,1,1]
	ds_write_b64 v13, v[42:43] offset:59136
	v_pk_mul_f32 v[42:43], v[180:181], v[16:17] op_sel:[1,1] op_sel_hi:[0,1] neg_lo:[0,1]
	v_pk_fma_f32 v[16:17], v[180:181], v[16:17], v[42:43] op_sel_hi:[1,0,1]
	v_pk_mul_f32 v[42:43], v[66:67], v[16:17] op_sel:[1,1] op_sel_hi:[1,0] neg_lo:[1,0]
	v_pk_fma_f32 v[42:43], v[66:67], v[16:17], v[42:43] op_sel_hi:[0,1,1]
	ds_write_b64 v13, v[42:43] offset:63360
	v_pk_mul_f32 v[42:43], v[180:181], v[16:17] op_sel:[1,1] op_sel_hi:[0,1] neg_lo:[0,1]
	v_pk_fma_f32 v[16:17], v[180:181], v[16:17], v[42:43] op_sel_hi:[1,0,1]
	v_sub_f32_e32 v10, v34, v35
	v_pk_mul_f32 v[34:35], v[16:17], s[46:47]
	v_pk_fma_f32 v[34:35], v[10:11], v[16:17], v[34:35] op_sel:[0,0,1] op_sel_hi:[0,1,0]
	v_add_u32_e32 v10, 0x10800, v13
	ds_write_b64 v10, v[34:35]
	v_pk_mul_f32 v[34:35], v[180:181], v[16:17] op_sel:[1,1] op_sel_hi:[0,1] neg_lo:[0,1]
	v_pk_fma_f32 v[16:17], v[180:181], v[16:17], v[34:35] op_sel_hi:[1,0,1]
	v_pk_mul_f32 v[34:35], v[54:55], v[16:17] op_sel:[1,1] op_sel_hi:[1,0] neg_lo:[1,0]
	v_add_u32_e32 v10, 0x11880, v13
	v_pk_fma_f32 v[34:35], v[54:55], v[16:17], v[34:35] op_sel_hi:[0,1,1]
	ds_write_b64 v10, v[34:35]
	v_pk_mul_f32 v[34:35], v[180:181], v[16:17] op_sel:[1,1] op_sel_hi:[0,1] neg_lo:[0,1]
	v_pk_fma_f32 v[16:17], v[180:181], v[16:17], v[34:35] op_sel_hi:[1,0,1]
	v_pk_mul_f32 v[34:35], v[38:39], v[16:17] op_sel:[1,1] op_sel_hi:[1,0] neg_lo:[1,0]
	v_add_u32_e32 v10, 0x12900, v13
	v_pk_fma_f32 v[34:35], v[38:39], v[16:17], v[34:35] op_sel_hi:[0,1,1]
	ds_write_b64 v10, v[34:35]
	v_pk_mul_f32 v[34:35], v[180:181], v[16:17] op_sel:[1,1] op_sel_hi:[0,1] neg_lo:[0,1]
	v_pk_fma_f32 v[16:17], v[180:181], v[16:17], v[34:35] op_sel_hi:[1,0,1]
	v_pk_mul_f32 v[34:35], v[56:57], v[16:17] op_sel:[1,1] op_sel_hi:[1,0] neg_lo:[1,0]
	v_add_u32_e32 v10, 0x13980, v13
	v_pk_fma_f32 v[34:35], v[56:57], v[16:17], v[34:35] op_sel_hi:[0,1,1]
	ds_write_b64 v10, v[34:35]
	v_pk_mul_f32 v[34:35], v[180:181], v[16:17] op_sel:[1,1] op_sel_hi:[0,1] neg_lo:[0,1]
	v_pk_fma_f32 v[16:17], v[180:181], v[16:17], v[34:35] op_sel_hi:[1,0,1]
	v_pk_mul_f32 v[34:35], v[30:31], v[16:17] op_sel:[1,1] op_sel_hi:[1,0] neg_lo:[1,0]
	v_add_u32_e32 v10, 0x14a00, v13
	v_pk_fma_f32 v[30:31], v[30:31], v[16:17], v[34:35] op_sel_hi:[0,1,1]
	ds_write_b64 v10, v[30:31]
	v_pk_mul_f32 v[30:31], v[180:181], v[16:17] op_sel:[1,1] op_sel_hi:[0,1] neg_lo:[0,1]
	v_pk_fma_f32 v[16:17], v[180:181], v[16:17], v[30:31] op_sel_hi:[1,0,1]
	v_pk_mul_f32 v[30:31], v[50:51], v[16:17] op_sel:[1,1] op_sel_hi:[1,0] neg_lo:[1,0]
	v_add_u32_e32 v10, 0x15a80, v13
	v_pk_fma_f32 v[30:31], v[50:51], v[16:17], v[30:31] op_sel_hi:[0,1,1]
	ds_write_b64 v10, v[30:31]
	v_pk_mul_f32 v[30:31], v[180:181], v[16:17] op_sel:[1,1] op_sel_hi:[0,1] neg_lo:[0,1]
	v_pk_fma_f32 v[16:17], v[180:181], v[16:17], v[30:31] op_sel_hi:[1,0,1]
	v_pk_mul_f32 v[30:31], v[32:33], v[16:17] op_sel:[1,1] op_sel_hi:[1,0] neg_lo:[1,0]
	v_add_u32_e32 v10, 0x16b00, v13
	v_pk_fma_f32 v[30:31], v[32:33], v[16:17], v[30:31] op_sel_hi:[0,1,1]
	ds_write_b64 v10, v[30:31]
	v_pk_mul_f32 v[30:31], v[180:181], v[16:17] op_sel:[1,1] op_sel_hi:[0,1] neg_lo:[0,1]
	v_pk_fma_f32 v[16:17], v[180:181], v[16:17], v[30:31] op_sel_hi:[1,0,1]
	v_pk_mul_f32 v[30:31], v[52:53], v[16:17] op_sel:[1,1] op_sel_hi:[1,0] neg_lo:[1,0]
	v_add_u32_e32 v10, 0x17b80, v13
	v_pk_fma_f32 v[30:31], v[52:53], v[16:17], v[30:31] op_sel_hi:[0,1,1]
	ds_write_b64 v10, v[30:31]
	v_pk_mul_f32 v[30:31], v[180:181], v[16:17] op_sel:[1,1] op_sel_hi:[0,1] neg_lo:[0,1]
	v_pk_fma_f32 v[16:17], v[180:181], v[16:17], v[30:31] op_sel_hi:[1,0,1]
	v_pk_mul_f32 v[30:31], v[24:25], v[16:17] op_sel:[1,1] op_sel_hi:[1,0] neg_lo:[1,0]
	v_add_u32_e32 v10, 0x18c00, v13
	v_pk_fma_f32 v[24:25], v[24:25], v[16:17], v[30:31] op_sel_hi:[0,1,1]
	ds_write_b64 v10, v[24:25]
	v_pk_mul_f32 v[24:25], v[180:181], v[16:17] op_sel:[1,1] op_sel_hi:[0,1] neg_lo:[0,1]
	v_pk_fma_f32 v[16:17], v[180:181], v[16:17], v[24:25] op_sel_hi:[1,0,1]
	v_pk_mul_f32 v[24:25], v[40:41], v[16:17] op_sel:[1,1] op_sel_hi:[1,0] neg_lo:[1,0]
	v_add_u32_e32 v10, 0x19c80, v13
	v_pk_fma_f32 v[24:25], v[40:41], v[16:17], v[24:25] op_sel_hi:[0,1,1]
	ds_write_b64 v10, v[24:25]
	v_pk_mul_f32 v[24:25], v[180:181], v[16:17] op_sel:[1,1] op_sel_hi:[0,1] neg_lo:[0,1]
	v_pk_fma_f32 v[16:17], v[180:181], v[16:17], v[24:25] op_sel_hi:[1,0,1]
	v_pk_mul_f32 v[24:25], v[26:27], v[16:17] op_sel:[1,1] op_sel_hi:[1,0] neg_lo:[1,0]
	v_add_u32_e32 v10, 0x1ad00, v13
	v_pk_fma_f32 v[24:25], v[26:27], v[16:17], v[24:25] op_sel_hi:[0,1,1]
	ds_write_b64 v10, v[24:25]
	v_pk_mul_f32 v[24:25], v[180:181], v[16:17] op_sel:[1,1] op_sel_hi:[0,1] neg_lo:[0,1]
	v_pk_fma_f32 v[16:17], v[180:181], v[16:17], v[24:25] op_sel_hi:[1,0,1]
	v_pk_mul_f32 v[24:25], v[44:45], v[16:17] op_sel:[1,1] op_sel_hi:[1,0] neg_lo:[1,0]
	v_add_u32_e32 v10, 0x1bd80, v13
	v_pk_fma_f32 v[24:25], v[44:45], v[16:17], v[24:25] op_sel_hi:[0,1,1]
	ds_write_b64 v10, v[24:25]
	v_pk_mul_f32 v[24:25], v[180:181], v[16:17] op_sel:[1,1] op_sel_hi:[0,1] neg_lo:[0,1]
	v_pk_fma_f32 v[16:17], v[180:181], v[16:17], v[24:25] op_sel_hi:[1,0,1]
	v_pk_mul_f32 v[24:25], v[20:21], v[16:17] op_sel:[1,1] op_sel_hi:[1,0] neg_lo:[1,0]
	v_add_u32_e32 v10, 0x1ce00, v13
	v_pk_fma_f32 v[20:21], v[20:21], v[16:17], v[24:25] op_sel_hi:[0,1,1]
	ds_write_b64 v10, v[20:21]
	v_pk_mul_f32 v[20:21], v[180:181], v[16:17] op_sel:[1,1] op_sel_hi:[0,1] neg_lo:[0,1]
	v_pk_fma_f32 v[16:17], v[180:181], v[16:17], v[20:21] op_sel_hi:[1,0,1]
	v_pk_mul_f32 v[20:21], v[36:37], v[16:17] op_sel:[1,1] op_sel_hi:[1,0] neg_lo:[1,0]
	v_add_u32_e32 v10, 0x1de80, v13
	v_pk_fma_f32 v[20:21], v[36:37], v[16:17], v[20:21] op_sel_hi:[0,1,1]
	ds_write_b64 v10, v[20:21]
	v_pk_mul_f32 v[20:21], v[180:181], v[16:17] op_sel:[1,1] op_sel_hi:[0,1] neg_lo:[0,1]
	v_pk_fma_f32 v[16:17], v[180:181], v[16:17], v[20:21] op_sel_hi:[1,0,1]
	v_pk_mul_f32 v[20:21], v[22:23], v[16:17] op_sel:[1,1] op_sel_hi:[1,0] neg_lo:[1,0]
	v_add_u32_e32 v10, 0x1ef00, v13
	v_pk_fma_f32 v[20:21], v[22:23], v[16:17], v[20:21] op_sel_hi:[0,1,1]
	ds_write_b64 v10, v[20:21]
	v_pk_mul_f32 v[20:21], v[180:181], v[16:17] op_sel:[1,1] op_sel_hi:[0,1] neg_lo:[0,1]
	v_pk_fma_f32 v[16:17], v[180:181], v[16:17], v[20:21] op_sel_hi:[1,0,1]
	v_pk_mul_f32 v[18:19], v[28:29], v[16:17] op_sel:[1,1] op_sel_hi:[1,0] neg_lo:[1,0]
	v_add_u32_e32 v10, 0x1ff80, v13
	v_pk_fma_f32 v[16:17], v[28:29], v[16:17], v[18:19] op_sel_hi:[0,1,1]
	ds_write_b64 v10, v[16:17]
	v_mov_b32_e32 v10, v176
	v_mov_b32_e32 v13, v173
	s_waitcnt lgkmcnt(0)
	s_barrier
	v_mov_b32_e32 v16, v182
	v_add_u32_e32 v15, v13, v10
	v_lshl_add_u32 v75, v15, 3, 0
	v_xad_u32 v15, v13, 1, v10
	v_lshl_add_u32 v74, v15, 3, 0
	v_xad_u32 v15, v13, 2, v10
	v_lshl_add_u32 v73, v15, 3, 0
	v_xad_u32 v15, v13, 3, v10
	v_lshl_add_u32 v72, v15, 3, 0
	v_xad_u32 v15, v13, 4, v10
	v_lshl_add_u32 v71, v15, 3, 0
	v_xad_u32 v15, v13, 5, v10
	v_lshl_add_u32 v70, v15, 3, 0
	v_xad_u32 v15, v13, 6, v10
	v_lshl_add_u32 v69, v15, 3, 0
	v_xad_u32 v15, v13, 7, v10
	v_lshl_add_u32 v68, v15, 3, 0
	v_xad_u32 v15, v13, 8, v10
	v_lshl_add_u32 v15, v15, 3, 0
	v_add_u32_e32 v67, 0x800, v15
	v_xad_u32 v15, v13, 9, v10
	v_lshl_add_u32 v15, v15, 3, 0
	v_add_u32_e32 v66, 0x800, v15
	v_xad_u32 v15, v13, 10, v10
	v_lshl_add_u32 v15, v15, 3, 0
	v_add_u32_e32 v65, 0x800, v15
	v_xad_u32 v15, v13, 11, v10
	v_lshl_add_u32 v15, v15, 3, 0
	v_add_u32_e32 v64, 0x800, v15
	v_xad_u32 v15, v13, 12, v10
	v_mov_b32_e32 v17, v183
	v_lshl_add_u32 v15, v15, 3, 0
	ds_read2_b64 v[18:21], v75 offset1:16
	ds_read2_b64 v[40:43], v67 offset1:16
	v_add_u32_e32 v63, 0x800, v15
	v_xad_u32 v15, v13, 13, v10
	v_lshl_add_u32 v15, v15, 3, 0
	v_add_u32_e32 v62, 0x800, v15
	v_xad_u32 v15, v13, 14, v10
	v_xad_u32 v10, v13, 15, v10
	ds_read2_b64 v[22:25], v74 offset0:32 offset1:48
	ds_read2_b64 v[48:51], v66 offset0:32 offset1:48
	v_lshl_add_u32 v15, v15, 3, 0
	v_lshl_add_u32 v10, v10, 3, 0
	v_add_u32_e32 v15, 0x800, v15
	v_add_u32_e32 v13, 0x800, v10
	v_mov_b32_e32 v10, v164
	ds_read2_b64 v[26:29], v73 offset0:64 offset1:80
	ds_read2_b64 v[58:61], v72 offset0:96 offset1:112
	ds_read2_b64 v[76:79], v71 offset0:128 offset1:144
	ds_read2_b64 v[80:83], v70 offset0:160 offset1:176
	ds_read2_b64 v[84:87], v69 offset0:192 offset1:208
	ds_read2_b64 v[88:91], v68 offset0:224 offset1:240
	ds_read2_b64 v[54:57], v65 offset0:64 offset1:80
	ds_read2_b64 v[92:95], v64 offset0:96 offset1:112
	ds_read2_b64 v[96:99], v63 offset0:128 offset1:144
	ds_read2_b64 v[100:103], v62 offset0:160 offset1:176
	ds_read2_b64 v[104:107], v15 offset0:192 offset1:208
	ds_read2_b64 v[108:111], v13 offset0:224 offset1:240
	s_waitcnt lgkmcnt(14)
	v_pk_add_f32 v[112:113], v[18:19], v[40:41]
	v_pk_add_f32 v[40:41], v[18:19], v[40:41] neg_lo:[0,1] neg_hi:[0,1]
	v_pk_add_f32 v[18:19], v[20:21], v[42:43]
	v_pk_add_f32 v[20:21], v[20:21], v[42:43] neg_lo:[0,1] neg_hi:[0,1]
	v_mov_b32_e32 v30, v165
	v_mov_b32_e32 v32, v166
	v_mov_b32_e32 v34, v167
	v_mov_b32_e32 v10, v168
	v_mov_b32_e32 v38, v169
	v_mov_b32_e32 v36, v170
	v_mov_b32_e32 v46, v171
	v_mov_b32_e32 v31, v172
	v_pk_mul_f32 v[42:43], v[20:21], v[46:47] op_sel:[1,0] op_sel_hi:[0,0] neg_lo:[1,1] neg_hi:[0,1]
	v_pk_fma_f32 v[44:45], v[20:21], v[30:31], v[42:43] op_sel_hi:[1,0,1]
	s_waitcnt lgkmcnt(12)
	v_pk_add_f32 v[20:21], v[22:23], v[48:49]
	v_pk_add_f32 v[22:23], v[22:23], v[48:49] neg_lo:[0,1] neg_hi:[0,1]
	v_pk_mul_f32 v[42:43], v[22:23], v[36:37] op_sel:[1,0] op_sel_hi:[0,0] neg_lo:[1,1] neg_hi:[0,1]
	v_pk_fma_f32 v[48:49], v[22:23], v[32:33], v[42:43] op_sel_hi:[1,0,1]
	v_pk_add_f32 v[22:23], v[24:25], v[50:51]
	v_pk_add_f32 v[24:25], v[24:25], v[50:51] neg_lo:[0,1] neg_hi:[0,1]
	v_pk_mul_f32 v[42:43], v[24:25], v[38:39] op_sel:[1,0] op_sel_hi:[0,0] neg_lo:[1,1] neg_hi:[0,1]
	v_pk_fma_f32 v[52:53], v[24:25], v[34:35], v[42:43] op_sel_hi:[1,0,1]
	s_waitcnt lgkmcnt(5)
	v_pk_add_f32 v[24:25], v[26:27], v[54:55]
	v_pk_add_f32 v[26:27], v[26:27], v[54:55] neg_lo:[0,1] neg_hi:[0,1]
	v_pk_mul_f32 v[42:43], v[26:27], v[10:11] op_sel:[1,0] op_sel_hi:[0,0] neg_lo:[1,1] neg_hi:[0,1]
	v_pk_fma_f32 v[54:55], v[26:27], v[10:11], v[42:43] op_sel_hi:[1,0,1]
	v_pk_add_f32 v[26:27], v[28:29], v[56:57]
	v_pk_add_f32 v[28:29], v[28:29], v[56:57] neg_lo:[0,1] neg_hi:[0,1]
	v_pk_mul_f32 v[42:43], v[28:29], v[38:39] op_sel_hi:[1,0]
	v_pk_fma_f32 v[56:57], v[28:29], v[34:35], v[42:43] op_sel:[1,0,0] op_sel_hi:[0,0,1] neg_lo:[1,1,0] neg_hi:[0,1,0]
	s_waitcnt lgkmcnt(4)
	v_pk_add_f32 v[42:43], v[58:59], v[92:93] neg_lo:[0,1] neg_hi:[0,1]
	v_pk_add_f32 v[28:29], v[58:59], v[92:93]
	v_pk_mul_f32 v[50:51], v[42:43], v[36:37] op_sel_hi:[1,0]
	v_pk_fma_f32 v[58:59], v[42:43], v[32:33], v[50:51] op_sel:[1,0,0] op_sel_hi:[0,0,1] neg_lo:[1,1,0] neg_hi:[0,1,0]
	v_pk_add_f32 v[50:51], v[60:61], v[94:95] neg_lo:[0,1] neg_hi:[0,1]
	v_pk_add_f32 v[42:43], v[60:61], v[94:95]
	v_pk_mul_f32 v[60:61], v[50:51], v[46:47] op_sel_hi:[1,0]
	v_xor_b32_e32 v92, 0x80000000, v51
	v_mov_b32_e32 v93, v50
	s_waitcnt lgkmcnt(3)
	v_pk_add_f32 v[50:51], v[76:77], v[96:97]
	v_pk_add_f32 v[76:77], v[76:77], v[96:97] neg_lo:[0,1] neg_hi:[0,1]
	v_pk_fma_f32 v[60:61], v[92:93], v[30:31], v[60:61] op_sel_hi:[1,0,1] neg_lo:[0,1,0] neg_hi:[0,1,0]
	v_xor_b32_e32 v93, 0x80000000, v76
	v_mov_b32_e32 v92, v77
	v_pk_add_f32 v[76:77], v[78:79], v[98:99]
	v_pk_add_f32 v[78:79], v[78:79], v[98:99] neg_lo:[0,1] neg_hi:[0,1]
	v_pk_mul_f32 v[94:95], v[78:79], v[46:47] op_sel_hi:[1,0] neg_lo:[0,1] neg_hi:[0,1]
	v_pk_fma_f32 v[78:79], v[78:79], v[30:31], v[94:95] op_sel:[1,0,0] op_sel_hi:[0,0,1] neg_lo:[1,1,0] neg_hi:[0,1,0]
	s_waitcnt lgkmcnt(2)
	v_pk_add_f32 v[94:95], v[80:81], v[100:101]
	v_pk_add_f32 v[80:81], v[80:81], v[100:101] neg_lo:[0,1] neg_hi:[0,1]
	v_pk_mul_f32 v[96:97], v[80:81], v[36:37] op_sel_hi:[1,0] neg_lo:[0,1] neg_hi:[0,1]
	v_pk_fma_f32 v[80:81], v[80:81], v[32:33], v[96:97] op_sel:[1,0,0] op_sel_hi:[0,0,1] neg_lo:[1,1,0] neg_hi:[0,1,0]
	v_pk_add_f32 v[96:97], v[82:83], v[102:103]
	v_pk_add_f32 v[82:83], v[82:83], v[102:103] neg_lo:[0,1] neg_hi:[0,1]
	v_pk_mul_f32 v[98:99], v[82:83], v[38:39] op_sel_hi:[1,0] neg_lo:[0,1] neg_hi:[0,1]
	v_pk_fma_f32 v[82:83], v[82:83], v[34:35], v[98:99] op_sel:[1,0,0] op_sel_hi:[0,0,1] neg_lo:[1,1,0] neg_hi:[0,1,0]
	s_waitcnt lgkmcnt(1)
	v_pk_add_f32 v[98:99], v[84:85], v[104:105]
	v_pk_add_f32 v[84:85], v[84:85], v[104:105] neg_lo:[0,1] neg_hi:[0,1]
	v_pk_mul_f32 v[100:101], v[84:85], v[10:11] op_sel:[1,0] op_sel_hi:[0,0] neg_lo:[1,1] neg_hi:[0,1]
	v_pk_fma_f32 v[84:85], v[84:85], v[10:11], v[100:101] op_sel_hi:[1,0,1] neg_lo:[0,1,0] neg_hi:[0,1,0]
	v_pk_add_f32 v[100:101], v[86:87], v[106:107]
	v_pk_add_f32 v[86:87], v[86:87], v[106:107] neg_lo:[0,1] neg_hi:[0,1]
	v_pk_mul_f32 v[38:39], v[86:87], v[38:39] op_sel:[1,0] op_sel_hi:[0,0] neg_lo:[1,1] neg_hi:[0,1]
	v_pk_fma_f32 v[86:87], v[86:87], v[34:35], v[38:39] op_sel_hi:[1,0,1] neg_lo:[0,1,0] neg_hi:[0,1,0]
	s_waitcnt lgkmcnt(0)
	v_pk_add_f32 v[38:39], v[88:89], v[108:109] neg_lo:[0,1] neg_hi:[0,1]
	v_pk_add_f32 v[34:35], v[88:89], v[108:109]
	v_pk_mul_f32 v[88:89], v[38:39], v[36:37] op_sel:[1,0] op_sel_hi:[0,0] neg_lo:[1,1] neg_hi:[0,1]
	v_pk_fma_f32 v[88:89], v[38:39], v[32:33], v[88:89] op_sel_hi:[1,0,1] neg_lo:[0,1,0] neg_hi:[0,1,0]
	v_pk_add_f32 v[38:39], v[90:91], v[110:111]
	v_pk_add_f32 v[90:91], v[90:91], v[110:111] neg_lo:[0,1] neg_hi:[0,1]
	v_pk_mul_f32 v[46:47], v[90:91], v[46:47] op_sel:[1,0] op_sel_hi:[0,0] neg_lo:[1,1] neg_hi:[0,1]
	v_pk_fma_f32 v[90:91], v[90:91], v[30:31], v[46:47] op_sel_hi:[1,0,1] neg_lo:[0,1,0] neg_hi:[0,1,0]
	v_pk_add_f32 v[46:47], v[18:19], v[76:77]
	v_pk_add_f32 v[18:19], v[18:19], v[76:77] neg_lo:[0,1] neg_hi:[0,1]
	v_pk_add_f32 v[30:31], v[112:113], v[50:51]
	v_pk_mul_f32 v[76:77], v[18:19], v[36:37] op_sel:[1,0] op_sel_hi:[0,0] neg_lo:[1,1] neg_hi:[0,1]
	v_pk_add_f32 v[50:51], v[112:113], v[50:51] neg_lo:[0,1] neg_hi:[0,1]
	v_pk_fma_f32 v[76:77], v[18:19], v[32:33], v[76:77] op_sel_hi:[1,0,1]
	v_pk_add_f32 v[18:19], v[20:21], v[94:95]
	v_pk_add_f32 v[20:21], v[20:21], v[94:95] neg_lo:[0,1] neg_hi:[0,1]
	v_pk_mul_f32 v[94:95], v[20:21], v[10:11] op_sel:[1,0] op_sel_hi:[0,0] neg_lo:[1,1] neg_hi:[0,1]
	v_pk_fma_f32 v[20:21], v[20:21], v[10:11], v[94:95] op_sel_hi:[1,0,1]
	v_pk_add_f32 v[94:95], v[22:23], v[96:97]
	v_pk_add_f32 v[22:23], v[22:23], v[96:97] neg_lo:[0,1] neg_hi:[0,1]
	v_pk_mul_f32 v[96:97], v[22:23], v[36:37] op_sel_hi:[1,0]
	v_xor_b32_e32 v102, 0x80000000, v23
	v_mov_b32_e32 v103, v22
	v_pk_add_f32 v[22:23], v[24:25], v[98:99]
	v_pk_add_f32 v[24:25], v[24:25], v[98:99] neg_lo:[0,1] neg_hi:[0,1]
	v_pk_fma_f32 v[96:97], v[102:103], v[32:33], v[96:97] op_sel_hi:[1,0,1] neg_lo:[0,1,0] neg_hi:[0,1,0]
	v_xor_b32_e32 v99, 0x80000000, v24
	v_mov_b32_e32 v98, v25
	v_pk_add_f32 v[24:25], v[26:27], v[100:101]
	v_pk_add_f32 v[26:27], v[26:27], v[100:101] neg_lo:[0,1] neg_hi:[0,1]
	v_pk_mul_f32 v[100:101], v[26:27], v[36:37] op_sel_hi:[1,0] neg_lo:[0,1] neg_hi:[0,1]
	v_xor_b32_e32 v102, 0x80000000, v27
	v_mov_b32_e32 v103, v26
	v_pk_add_f32 v[26:27], v[28:29], v[34:35]
	v_pk_add_f32 v[28:29], v[28:29], v[34:35] neg_lo:[0,1] neg_hi:[0,1]
	v_pk_fma_f32 v[100:101], v[102:103], v[32:33], v[100:101] op_sel_hi:[1,0,1] neg_lo:[0,1,0] neg_hi:[0,1,0]
	v_pk_mul_f32 v[34:35], v[28:29], v[10:11] op_sel:[1,0] op_sel_hi:[0,0] neg_lo:[1,1] neg_hi:[0,1]
	v_pk_add_f32 v[102:103], v[30:31], v[22:23] neg_lo:[0,1] neg_hi:[0,1]
	v_pk_fma_f32 v[28:29], v[28:29], v[10:11], v[34:35] op_sel_hi:[1,0,1] neg_lo:[0,1,0] neg_hi:[0,1,0]
	v_pk_add_f32 v[34:35], v[42:43], v[38:39]
	v_pk_add_f32 v[38:39], v[42:43], v[38:39] neg_lo:[0,1] neg_hi:[0,1]
	v_pk_mul_f32 v[42:43], v[38:39], v[36:37] op_sel:[1,0] op_sel_hi:[0,0] neg_lo:[1,1] neg_hi:[0,1]
	v_pk_fma_f32 v[42:43], v[38:39], v[32:33], v[42:43] op_sel_hi:[1,0,1] neg_lo:[0,1,0] neg_hi:[0,1,0]
	v_pk_add_f32 v[38:39], v[30:31], v[22:23]
	v_pk_add_f32 v[22:23], v[46:47], v[24:25]
	v_pk_add_f32 v[24:25], v[46:47], v[24:25] neg_lo:[0,1] neg_hi:[0,1]
	v_pk_mul_f32 v[30:31], v[24:25], v[10:11] op_sel:[1,0] op_sel_hi:[0,0] neg_lo:[1,1] neg_hi:[0,1]
	v_pk_fma_f32 v[24:25], v[24:25], v[10:11], v[30:31] op_sel_hi:[1,0,1]
	v_pk_add_f32 v[30:31], v[18:19], v[26:27]
	v_pk_add_f32 v[18:19], v[18:19], v[26:27] neg_lo:[0,1] neg_hi:[0,1]
	v_xor_b32_e32 v27, 0x80000000, v18
	v_mov_b32_e32 v26, v19
	v_pk_add_f32 v[18:19], v[94:95], v[34:35]
	v_pk_add_f32 v[34:35], v[94:95], v[34:35] neg_lo:[0,1] neg_hi:[0,1]
	v_pk_mul_f32 v[46:47], v[34:35], v[10:11] op_sel:[1,0] op_sel_hi:[0,0] neg_lo:[1,1] neg_hi:[0,1]
	v_pk_fma_f32 v[34:35], v[34:35], v[10:11], v[46:47] op_sel_hi:[1,0,1] neg_lo:[0,1,0] neg_hi:[0,1,0]
	v_pk_add_f32 v[46:47], v[38:39], v[30:31]
	v_pk_add_f32 v[38:39], v[38:39], v[30:31] neg_lo:[0,1] neg_hi:[0,1]
	v_pk_add_f32 v[30:31], v[22:23], v[18:19]
	v_pk_add_f32 v[18:19], v[22:23], v[18:19] neg_lo:[0,1] neg_hi:[0,1]
	v_pk_add_f32 v[94:95], v[46:47], v[30:31]
	v_xor_b32_e32 v23, 0x80000000, v18
	v_mov_b32_e32 v22, v19
	v_pk_add_f32 v[18:19], v[102:103], v[26:27]
	v_pk_add_f32 v[102:103], v[102:103], v[26:27] neg_lo:[0,1] neg_hi:[0,1]
	v_pk_add_f32 v[26:27], v[24:25], v[34:35]
	v_pk_add_f32 v[24:25], v[24:25], v[34:35] neg_lo:[0,1] neg_hi:[0,1]
	v_pk_add_f32 v[30:31], v[46:47], v[30:31] neg_lo:[0,1] neg_hi:[0,1]
	v_xor_b32_e32 v35, 0x80000000, v24
	v_mov_b32_e32 v34, v25
	v_pk_add_f32 v[24:25], v[50:51], v[98:99]
	v_pk_add_f32 v[98:99], v[50:51], v[98:99] neg_lo:[0,1] neg_hi:[0,1]
	v_pk_add_f32 v[50:51], v[76:77], v[100:101] neg_lo:[0,1] neg_hi:[0,1]
	v_pk_add_f32 v[46:47], v[38:39], v[22:23]
	v_pk_add_f32 v[22:23], v[38:39], v[22:23] neg_lo:[0,1] neg_hi:[0,1]
	v_pk_add_f32 v[104:105], v[18:19], v[26:27]
	v_pk_add_f32 v[26:27], v[18:19], v[26:27] neg_lo:[0,1] neg_hi:[0,1]
	v_pk_add_f32 v[38:39], v[102:103], v[34:35]
	v_pk_add_f32 v[18:19], v[102:103], v[34:35] neg_lo:[0,1] neg_hi:[0,1]
	v_pk_add_f32 v[34:35], v[76:77], v[100:101]
	v_pk_mul_f32 v[76:77], v[10:11], v[50:51] op_sel:[0,1] op_sel_hi:[0,0] neg_lo:[1,1] neg_hi:[1,0]
	v_pk_fma_f32 v[76:77], v[10:11], v[50:51], v[76:77] op_sel_hi:[0,1,1]
	v_pk_add_f32 v[50:51], v[20:21], v[28:29]
	v_pk_add_f32 v[20:21], v[20:21], v[28:29] neg_lo:[0,1] neg_hi:[0,1]
	v_xor_b32_e32 v29, 0x80000000, v20
	v_mov_b32_e32 v28, v21
	v_pk_add_f32 v[20:21], v[96:97], v[42:43]
	v_pk_add_f32 v[42:43], v[96:97], v[42:43] neg_lo:[0,1] neg_hi:[0,1]
	v_pk_mul_f32 v[96:97], v[10:11], v[42:43] op_sel:[0,1] op_sel_hi:[0,0] neg_lo:[1,1] neg_hi:[1,0]
	v_pk_fma_f32 v[42:43], v[10:11], v[42:43], v[96:97] op_sel_hi:[0,1,1] neg_lo:[1,0,0] neg_hi:[1,0,0]
	v_pk_add_f32 v[96:97], v[24:25], v[50:51]
	v_pk_add_f32 v[24:25], v[24:25], v[50:51] neg_lo:[0,1] neg_hi:[0,1]
	v_pk_add_f32 v[50:51], v[34:35], v[20:21]
	v_pk_add_f32 v[20:21], v[34:35], v[20:21] neg_lo:[0,1] neg_hi:[0,1]
	v_pk_add_f32 v[102:103], v[96:97], v[50:51]
	v_xor_b32_e32 v101, 0x80000000, v20
	v_mov_b32_e32 v100, v21
	v_pk_add_f32 v[34:35], v[96:97], v[50:51] neg_lo:[0,1] neg_hi:[0,1]
	v_pk_add_f32 v[20:21], v[98:99], v[28:29]
	v_pk_add_f32 v[96:97], v[98:99], v[28:29] neg_lo:[0,1] neg_hi:[0,1]
	v_pk_add_f32 v[28:29], v[76:77], v[42:43]
	v_pk_add_f32 v[42:43], v[76:77], v[42:43] neg_lo:[0,1] neg_hi:[0,1]
	v_pk_add_f32 v[98:99], v[20:21], v[28:29]
	v_xor_b32_e32 v77, 0x80000000, v42
	v_mov_b32_e32 v76, v43
	v_pk_add_f32 v[28:29], v[20:21], v[28:29] neg_lo:[0,1] neg_hi:[0,1]
	v_pk_add_f32 v[42:43], v[96:97], v[76:77]
	v_pk_add_f32 v[20:21], v[96:97], v[76:77] neg_lo:[0,1] neg_hi:[0,1]
	v_pk_add_f32 v[76:77], v[40:41], v[92:93]
	v_pk_add_f32 v[92:93], v[40:41], v[92:93] neg_lo:[0,1] neg_hi:[0,1]
	v_pk_add_f32 v[40:41], v[44:45], v[78:79]
	v_pk_add_f32 v[44:45], v[44:45], v[78:79] neg_lo:[0,1] neg_hi:[0,1]
	v_pk_add_f32 v[50:51], v[24:25], v[100:101]
	v_pk_mul_f32 v[78:79], v[36:37], v[44:45] op_sel:[0,1] op_sel_hi:[0,0] neg_lo:[1,1] neg_hi:[1,0]
	v_pk_fma_f32 v[44:45], v[32:33], v[44:45], v[78:79] op_sel_hi:[0,1,1]
	v_pk_add_f32 v[78:79], v[48:49], v[80:81]
	v_pk_add_f32 v[48:49], v[48:49], v[80:81] neg_lo:[0,1] neg_hi:[0,1]
	v_pk_add_f32 v[24:25], v[24:25], v[100:101] neg_lo:[0,1] neg_hi:[0,1]
	v_pk_mul_f32 v[80:81], v[10:11], v[48:49] op_sel:[0,1] op_sel_hi:[0,0] neg_lo:[1,1] neg_hi:[1,0]
	v_pk_fma_f32 v[80:81], v[10:11], v[48:49], v[80:81] op_sel_hi:[0,1,1]
	v_pk_add_f32 v[48:49], v[52:53], v[82:83]
	v_pk_add_f32 v[52:53], v[52:53], v[82:83] neg_lo:[0,1] neg_hi:[0,1]
	v_pk_mul_f32 v[82:83], v[32:33], v[52:53] op_sel:[0,1] op_sel_hi:[0,0] neg_lo:[1,1] neg_hi:[1,0]
	v_pk_fma_f32 v[52:53], v[36:37], v[52:53], v[82:83] op_sel_hi:[0,1,1]
	v_pk_add_f32 v[82:83], v[54:55], v[84:85]
	v_pk_add_f32 v[54:55], v[54:55], v[84:85] neg_lo:[0,1] neg_hi:[0,1]
	v_xor_b32_e32 v85, 0x80000000, v54
	v_mov_b32_e32 v84, v55
	v_pk_add_f32 v[54:55], v[56:57], v[86:87]
	v_pk_add_f32 v[56:57], v[56:57], v[86:87] neg_lo:[0,1] neg_hi:[0,1]
	v_pk_mul_f32 v[86:87], v[32:33], v[56:57] op_sel:[0,1] op_sel_hi:[0,0] neg_lo:[1,1] neg_hi:[1,0]
	v_pk_fma_f32 v[56:57], v[36:37], v[56:57], v[86:87] op_sel_hi:[0,1,1] neg_lo:[1,0,0] neg_hi:[1,0,0]
	v_pk_add_f32 v[86:87], v[58:59], v[88:89]
	v_pk_add_f32 v[58:59], v[58:59], v[88:89] neg_lo:[0,1] neg_hi:[0,1]
	v_pk_mul_f32 v[88:89], v[10:11], v[58:59] op_sel:[0,1] op_sel_hi:[0,0] neg_lo:[1,1] neg_hi:[1,0]
	v_pk_fma_f32 v[58:59], v[10:11], v[58:59], v[88:89] op_sel_hi:[0,1,1] neg_lo:[1,0,0] neg_hi:[1,0,0]
	v_pk_add_f32 v[88:89], v[60:61], v[90:91]
	v_pk_add_f32 v[60:61], v[60:61], v[90:91] neg_lo:[0,1] neg_hi:[0,1]
	v_pk_mul_f32 v[36:37], v[36:37], v[60:61] op_sel:[0,1] op_sel_hi:[0,0] neg_lo:[1,1] neg_hi:[1,0]
	v_pk_fma_f32 v[36:37], v[32:33], v[60:61], v[36:37] op_sel_hi:[0,1,1] neg_lo:[1,0,0] neg_hi:[1,0,0]
	v_pk_add_f32 v[32:33], v[76:77], v[82:83]
	v_pk_add_f32 v[60:61], v[76:77], v[82:83] neg_lo:[0,1] neg_hi:[0,1]
	v_pk_add_f32 v[76:77], v[54:55], v[40:41]
	v_pk_add_f32 v[40:41], v[40:41], v[54:55] neg_lo:[0,1] neg_hi:[0,1]
	v_pk_mul_f32 v[54:55], v[10:11], v[40:41] op_sel:[0,1] op_sel_hi:[0,0] neg_lo:[1,1] neg_hi:[1,0]
	v_pk_fma_f32 v[54:55], v[10:11], v[40:41], v[54:55] op_sel_hi:[0,1,1]
	v_pk_add_f32 v[40:41], v[78:79], v[86:87]
	v_pk_add_f32 v[78:79], v[78:79], v[86:87] neg_lo:[0,1] neg_hi:[0,1]
	v_xor_b32_e32 v83, 0x80000000, v78
	v_mov_b32_e32 v82, v79
	v_pk_add_f32 v[78:79], v[48:49], v[88:89]
	v_pk_add_f32 v[48:49], v[48:49], v[88:89] neg_lo:[0,1] neg_hi:[0,1]
	v_pk_add_f32 v[88:89], v[76:77], v[78:79]
	v_pk_mul_f32 v[86:87], v[10:11], v[48:49] op_sel:[0,1] op_sel_hi:[0,0] neg_lo:[1,1] neg_hi:[1,0]
	v_pk_fma_f32 v[48:49], v[10:11], v[48:49], v[86:87] op_sel_hi:[0,1,1] neg_lo:[1,0,0] neg_hi:[1,0,0]
	v_pk_add_f32 v[86:87], v[32:33], v[40:41]
	v_pk_add_f32 v[32:33], v[32:33], v[40:41] neg_lo:[0,1] neg_hi:[0,1]
	v_pk_add_f32 v[40:41], v[76:77], v[78:79] neg_lo:[0,1] neg_hi:[0,1]
	v_pk_add_f32 v[78:79], v[86:87], v[88:89] neg_lo:[0,1] neg_hi:[0,1]
	v_pk_add_f32 v[90:91], v[32:33], v[40:41] op_sel:[0,1] op_sel_hi:[1,0] neg_hi:[0,1]
	v_pk_add_f32 v[40:41], v[32:33], v[40:41] op_sel:[0,1] op_sel_hi:[1,0] neg_lo:[0,1]
	v_pk_add_f32 v[76:77], v[54:55], v[48:49]
	v_pk_add_f32 v[48:49], v[54:55], v[48:49] neg_lo:[0,1] neg_hi:[0,1]
	v_pk_add_f32 v[32:33], v[60:61], v[82:83]
	v_pk_add_f32 v[60:61], v[60:61], v[82:83] neg_lo:[0,1] neg_hi:[0,1]
	v_xor_b32_e32 v55, 0x80000000, v48
	v_mov_b32_e32 v54, v49
	v_pk_add_f32 v[82:83], v[32:33], v[76:77]
	v_pk_add_f32 v[48:49], v[32:33], v[76:77] neg_lo:[0,1] neg_hi:[0,1]
	v_pk_add_f32 v[76:77], v[60:61], v[54:55]
	v_pk_add_f32 v[32:33], v[60:61], v[54:55] neg_lo:[0,1] neg_hi:[0,1]
	v_pk_add_f32 v[54:55], v[92:93], v[84:85]
	v_pk_add_f32 v[60:61], v[92:93], v[84:85] neg_lo:[0,1] neg_hi:[0,1]
	v_pk_add_f32 v[84:85], v[56:57], v[44:45]
	v_pk_add_f32 v[44:45], v[44:45], v[56:57] neg_lo:[0,1] neg_hi:[0,1]
	v_pk_add_f32 v[86:87], v[86:87], v[88:89]
	v_pk_mul_f32 v[56:57], v[10:11], v[44:45] op_sel:[0,1] op_sel_hi:[0,0] neg_lo:[1,1] neg_hi:[1,0]
	v_pk_fma_f32 v[56:57], v[10:11], v[44:45], v[56:57] op_sel_hi:[0,1,1]
	v_pk_add_f32 v[44:45], v[80:81], v[58:59]
	v_pk_add_f32 v[58:59], v[80:81], v[58:59] neg_lo:[0,1] neg_hi:[0,1]
	v_xor_b32_e32 v81, 0x80000000, v58
	v_mov_b32_e32 v80, v59
	v_pk_add_f32 v[58:59], v[52:53], v[36:37]
	v_pk_add_f32 v[36:37], v[52:53], v[36:37] neg_lo:[0,1] neg_hi:[0,1]
	v_pk_mul_f32 v[52:53], v[10:11], v[36:37] op_sel:[0,1] op_sel_hi:[0,0] neg_lo:[1,1] neg_hi:[1,0]
	v_pk_fma_f32 v[36:37], v[10:11], v[36:37], v[52:53] op_sel_hi:[0,1,1] neg_lo:[1,0,0] neg_hi:[1,0,0]
	v_pk_add_f32 v[52:53], v[54:55], v[44:45]
	v_pk_add_f32 v[44:45], v[54:55], v[44:45] neg_lo:[0,1] neg_hi:[0,1]
	v_pk_add_f32 v[54:55], v[84:85], v[58:59]
	v_pk_add_f32 v[58:59], v[84:85], v[58:59] neg_lo:[0,1] neg_hi:[0,1]
	v_xor_b32_e32 v85, 0x80000000, v58
	v_mov_b32_e32 v84, v59
	v_pk_add_f32 v[58:59], v[52:53], v[54:55]
	v_pk_add_f32 v[52:53], v[52:53], v[54:55] neg_lo:[0,1] neg_hi:[0,1]
	v_pk_add_f32 v[54:55], v[44:45], v[84:85]
	v_pk_add_f32 v[44:45], v[44:45], v[84:85] neg_lo:[0,1] neg_hi:[0,1]
	v_pk_add_f32 v[84:85], v[60:61], v[80:81]
	v_pk_add_f32 v[60:61], v[60:61], v[80:81] neg_lo:[0,1] neg_hi:[0,1]
	v_pk_add_f32 v[80:81], v[56:57], v[36:37]
	v_pk_add_f32 v[36:37], v[56:57], v[36:37] neg_lo:[0,1] neg_hi:[0,1]
	v_pk_add_f32 v[92:93], v[84:85], v[80:81]
	v_pk_add_f32 v[80:81], v[84:85], v[80:81] neg_lo:[0,1] neg_hi:[0,1]
	v_pk_add_f32 v[84:85], v[60:61], v[36:37] op_sel:[0,1] op_sel_hi:[1,0] neg_hi:[0,1]
	v_pk_add_f32 v[36:37], v[60:61], v[36:37] op_sel:[0,1] op_sel_hi:[1,0] neg_lo:[0,1]
	v_pk_fma_f32 v[60:61], v[16:17], s[92:93], v[16:17] op_sel:[1,0,0] op_sel_hi:[0,1,1]
	v_pk_mul_f32 v[56:57], v[94:95], s[14:15] op_sel:[1,0] neg_lo:[1,0]
	v_pk_mul_f32 v[88:89], v[60:61], v[86:87] op_sel:[1,1] op_sel_hi:[0,1] neg_lo:[0,1]
	v_pk_fma_f32 v[56:57], v[94:95], s[42:43], v[56:57] op_sel_hi:[0,1,1]
	v_pk_fma_f32 v[86:87], v[60:61], v[86:87], v[88:89] op_sel_hi:[1,0,1]
	ds_write2_b64 v75, v[56:57], v[86:87] offset1:16
	v_pk_mul_f32 v[56:57], v[16:17], v[60:61] op_sel:[1,1] op_sel_hi:[0,1] neg_lo:[0,1]
	v_pk_fma_f32 v[56:57], v[16:17], v[60:61], v[56:57] op_sel_hi:[1,0,1]
	v_pk_mul_f32 v[60:61], v[56:57], v[102:103] op_sel:[1,1] op_sel_hi:[0,1] neg_lo:[0,1]
	v_pk_mul_f32 v[86:87], v[16:17], v[56:57] op_sel:[1,1] op_sel_hi:[0,1] neg_lo:[0,1]
	v_pk_fma_f32 v[60:61], v[56:57], v[102:103], v[60:61] op_sel_hi:[1,0,1]
	v_pk_fma_f32 v[56:57], v[16:17], v[56:57], v[86:87] op_sel_hi:[1,0,1]
	v_pk_mul_f32 v[86:87], v[56:57], v[58:59] op_sel:[1,1] op_sel_hi:[0,1] neg_lo:[0,1]
	v_pk_fma_f32 v[58:59], v[56:57], v[58:59], v[86:87] op_sel_hi:[1,0,1]
	ds_write2_b64 v74, v[60:61], v[58:59] offset0:32 offset1:48
	v_pk_mul_f32 v[58:59], v[16:17], v[56:57] op_sel:[1,1] op_sel_hi:[0,1] neg_lo:[0,1]
	v_pk_fma_f32 v[56:57], v[16:17], v[56:57], v[58:59] op_sel_hi:[1,0,1]
	v_pk_mul_f32 v[58:59], v[56:57], v[104:105] op_sel:[1,1] op_sel_hi:[0,1] neg_lo:[0,1]
	v_pk_mul_f32 v[60:61], v[16:17], v[56:57] op_sel:[1,1] op_sel_hi:[0,1] neg_lo:[0,1]
	v_pk_fma_f32 v[58:59], v[56:57], v[104:105], v[58:59] op_sel_hi:[1,0,1]
	v_pk_fma_f32 v[56:57], v[16:17], v[56:57], v[60:61] op_sel_hi:[1,0,1]
	v_pk_mul_f32 v[60:61], v[56:57], v[82:83] op_sel:[1,1] op_sel_hi:[0,1] neg_lo:[0,1]
	v_pk_fma_f32 v[60:61], v[56:57], v[82:83], v[60:61] op_sel_hi:[1,0,1]
	ds_write2_b64 v73, v[58:59], v[60:61] offset0:64 offset1:80
	v_pk_mul_f32 v[58:59], v[16:17], v[56:57] op_sel:[1,1] op_sel_hi:[0,1] neg_lo:[0,1]
	v_pk_fma_f32 v[56:57], v[16:17], v[56:57], v[58:59] op_sel_hi:[1,0,1]
	v_pk_mul_f32 v[58:59], v[56:57], v[98:99] op_sel:[1,1] op_sel_hi:[0,1] neg_lo:[0,1]
	v_pk_mul_f32 v[60:61], v[16:17], v[56:57] op_sel:[1,1] op_sel_hi:[0,1] neg_lo:[0,1]
	v_pk_fma_f32 v[58:59], v[56:57], v[98:99], v[58:59] op_sel_hi:[1,0,1]
	v_pk_fma_f32 v[56:57], v[16:17], v[56:57], v[60:61] op_sel_hi:[1,0,1]
	v_pk_mul_f32 v[60:61], v[56:57], v[92:93] op_sel:[1,1] op_sel_hi:[0,1] neg_lo:[0,1]
	v_pk_fma_f32 v[60:61], v[56:57], v[92:93], v[60:61] op_sel_hi:[1,0,1]
	ds_write2_b64 v72, v[58:59], v[60:61] offset0:96 offset1:112
	v_pk_mul_f32 v[58:59], v[16:17], v[56:57] op_sel:[1,1] op_sel_hi:[0,1] neg_lo:[0,1]
	v_pk_fma_f32 v[56:57], v[16:17], v[56:57], v[58:59] op_sel_hi:[1,0,1]
	v_pk_mul_f32 v[58:59], v[56:57], v[46:47] op_sel:[1,1] op_sel_hi:[0,1] neg_lo:[0,1]
	v_pk_fma_f32 v[46:47], v[56:57], v[46:47], v[58:59] op_sel_hi:[1,0,1]
	v_pk_mul_f32 v[58:59], v[16:17], v[56:57] op_sel:[1,1] op_sel_hi:[0,1] neg_lo:[0,1]
	v_pk_fma_f32 v[56:57], v[16:17], v[56:57], v[58:59] op_sel_hi:[1,0,1]
	v_pk_mul_f32 v[58:59], v[56:57], v[90:91] op_sel:[1,1] op_sel_hi:[0,1] neg_lo:[0,1]
	v_pk_fma_f32 v[58:59], v[56:57], v[90:91], v[58:59] op_sel_hi:[1,0,1]
	ds_write2_b64 v71, v[46:47], v[58:59] offset0:128 offset1:144
	v_pk_mul_f32 v[46:47], v[16:17], v[56:57] op_sel:[1,1] op_sel_hi:[0,1] neg_lo:[0,1]
	v_pk_fma_f32 v[46:47], v[16:17], v[56:57], v[46:47] op_sel_hi:[1,0,1]
	v_pk_mul_f32 v[56:57], v[46:47], v[50:51] op_sel:[1,1] op_sel_hi:[0,1] neg_lo:[0,1]
	v_pk_fma_f32 v[50:51], v[46:47], v[50:51], v[56:57] op_sel_hi:[1,0,1]
	v_pk_mul_f32 v[56:57], v[16:17], v[46:47] op_sel:[1,1] op_sel_hi:[0,1] neg_lo:[0,1]
	v_pk_fma_f32 v[46:47], v[16:17], v[46:47], v[56:57] op_sel_hi:[1,0,1]
	v_pk_mul_f32 v[56:57], v[46:47], v[54:55] op_sel:[1,1] op_sel_hi:[0,1] neg_lo:[0,1]
	v_pk_fma_f32 v[54:55], v[46:47], v[54:55], v[56:57] op_sel_hi:[1,0,1]
	ds_write2_b64 v70, v[50:51], v[54:55] offset0:160 offset1:176
	v_pk_mul_f32 v[50:51], v[16:17], v[46:47] op_sel:[1,1] op_sel_hi:[0,1] neg_lo:[0,1]
	v_pk_fma_f32 v[46:47], v[16:17], v[46:47], v[50:51] op_sel_hi:[1,0,1]
	v_pk_mul_f32 v[50:51], v[38:39], v[46:47] op_sel:[1,1] op_sel_hi:[1,0] neg_lo:[1,0]
	v_pk_fma_f32 v[38:39], v[38:39], v[46:47], v[50:51] op_sel_hi:[0,1,1]
	v_pk_mul_f32 v[50:51], v[16:17], v[46:47] op_sel:[1,1] op_sel_hi:[0,1] neg_lo:[0,1]
	v_pk_fma_f32 v[46:47], v[16:17], v[46:47], v[50:51] op_sel_hi:[1,0,1]
	v_pk_mul_f32 v[50:51], v[46:47], v[76:77] op_sel:[1,1] op_sel_hi:[0,1] neg_lo:[0,1]
	v_pk_fma_f32 v[50:51], v[46:47], v[76:77], v[50:51] op_sel_hi:[1,0,1]
	ds_write2_b64 v69, v[38:39], v[50:51] offset0:192 offset1:208
	v_pk_mul_f32 v[38:39], v[16:17], v[46:47] op_sel:[1,1] op_sel_hi:[0,1] neg_lo:[0,1]
	v_pk_fma_f32 v[38:39], v[16:17], v[46:47], v[38:39] op_sel_hi:[1,0,1]
	v_pk_mul_f32 v[46:47], v[42:43], v[38:39] op_sel:[1,1] op_sel_hi:[1,0] neg_lo:[1,0]
	v_pk_fma_f32 v[42:43], v[42:43], v[38:39], v[46:47] op_sel_hi:[0,1,1]
	v_pk_mul_f32 v[46:47], v[16:17], v[38:39] op_sel:[1,1] op_sel_hi:[0,1] neg_lo:[0,1]
	v_pk_fma_f32 v[38:39], v[16:17], v[38:39], v[46:47] op_sel_hi:[1,0,1]
	v_pk_mul_f32 v[46:47], v[38:39], v[84:85] op_sel:[1,1] op_sel_hi:[0,1] neg_lo:[0,1]
	v_pk_fma_f32 v[46:47], v[38:39], v[84:85], v[46:47] op_sel_hi:[1,0,1]
	ds_write2_b64 v68, v[42:43], v[46:47] offset0:224 offset1:240
	v_pk_mul_f32 v[42:43], v[16:17], v[38:39] op_sel:[1,1] op_sel_hi:[0,1] neg_lo:[0,1]
	v_pk_fma_f32 v[38:39], v[16:17], v[38:39], v[42:43] op_sel_hi:[1,0,1]
	v_pk_mul_f32 v[42:43], v[30:31], v[38:39] op_sel:[1,1] op_sel_hi:[1,0] neg_lo:[1,0]
	v_pk_fma_f32 v[30:31], v[30:31], v[38:39], v[42:43] op_sel_hi:[0,1,1]
	v_pk_mul_f32 v[42:43], v[16:17], v[38:39] op_sel:[1,1] op_sel_hi:[0,1] neg_lo:[0,1]
	v_pk_fma_f32 v[38:39], v[16:17], v[38:39], v[42:43] op_sel_hi:[1,0,1]
	v_pk_mul_f32 v[42:43], v[78:79], v[38:39] op_sel:[1,1] op_sel_hi:[1,0] neg_lo:[1,0]
	v_pk_fma_f32 v[42:43], v[78:79], v[38:39], v[42:43] op_sel_hi:[0,1,1]
	ds_write2_b64 v67, v[30:31], v[42:43] offset1:16
	v_pk_mul_f32 v[30:31], v[16:17], v[38:39] op_sel:[1,1] op_sel_hi:[0,1] neg_lo:[0,1]
	v_pk_fma_f32 v[30:31], v[16:17], v[38:39], v[30:31] op_sel_hi:[1,0,1]
	v_pk_mul_f32 v[38:39], v[34:35], v[30:31] op_sel:[1,1] op_sel_hi:[1,0] neg_lo:[1,0]
	v_pk_fma_f32 v[34:35], v[34:35], v[30:31], v[38:39] op_sel_hi:[0,1,1]
	v_pk_mul_f32 v[38:39], v[16:17], v[30:31] op_sel:[1,1] op_sel_hi:[0,1] neg_lo:[0,1]
	v_pk_fma_f32 v[30:31], v[16:17], v[30:31], v[38:39] op_sel_hi:[1,0,1]
	v_pk_mul_f32 v[38:39], v[52:53], v[30:31] op_sel:[1,1] op_sel_hi:[1,0] neg_lo:[1,0]
	v_pk_fma_f32 v[38:39], v[52:53], v[30:31], v[38:39] op_sel_hi:[0,1,1]
	ds_write2_b64 v66, v[34:35], v[38:39] offset0:32 offset1:48
	v_pk_mul_f32 v[34:35], v[16:17], v[30:31] op_sel:[1,1] op_sel_hi:[0,1] neg_lo:[0,1]
	v_pk_fma_f32 v[30:31], v[16:17], v[30:31], v[34:35] op_sel_hi:[1,0,1]
	v_pk_mul_f32 v[34:35], v[26:27], v[30:31] op_sel:[1,1] op_sel_hi:[1,0] neg_lo:[1,0]
	v_pk_fma_f32 v[26:27], v[26:27], v[30:31], v[34:35] op_sel_hi:[0,1,1]
	v_pk_mul_f32 v[34:35], v[16:17], v[30:31] op_sel:[1,1] op_sel_hi:[0,1] neg_lo:[0,1]
	v_pk_fma_f32 v[30:31], v[16:17], v[30:31], v[34:35] op_sel_hi:[1,0,1]
	v_pk_mul_f32 v[34:35], v[48:49], v[30:31] op_sel:[1,1] op_sel_hi:[1,0] neg_lo:[1,0]
	v_pk_fma_f32 v[34:35], v[48:49], v[30:31], v[34:35] op_sel_hi:[0,1,1]
	ds_write2_b64 v65, v[26:27], v[34:35] offset0:64 offset1:80
	v_pk_mul_f32 v[26:27], v[16:17], v[30:31] op_sel:[1,1] op_sel_hi:[0,1] neg_lo:[0,1]
	v_pk_fma_f32 v[26:27], v[16:17], v[30:31], v[26:27] op_sel_hi:[1,0,1]
	v_pk_mul_f32 v[30:31], v[28:29], v[26:27] op_sel:[1,1] op_sel_hi:[1,0] neg_lo:[1,0]
	v_pk_fma_f32 v[28:29], v[28:29], v[26:27], v[30:31] op_sel_hi:[0,1,1]
	v_pk_mul_f32 v[30:31], v[16:17], v[26:27] op_sel:[1,1] op_sel_hi:[0,1] neg_lo:[0,1]
	v_pk_fma_f32 v[26:27], v[16:17], v[26:27], v[30:31] op_sel_hi:[1,0,1]
	v_pk_mul_f32 v[30:31], v[80:81], v[26:27] op_sel:[1,1] op_sel_hi:[1,0] neg_lo:[1,0]
	v_pk_fma_f32 v[30:31], v[80:81], v[26:27], v[30:31] op_sel_hi:[0,1,1]
	ds_write2_b64 v64, v[28:29], v[30:31] offset0:96 offset1:112
	v_pk_mul_f32 v[28:29], v[16:17], v[26:27] op_sel:[1,1] op_sel_hi:[0,1] neg_lo:[0,1]
	v_pk_fma_f32 v[26:27], v[16:17], v[26:27], v[28:29] op_sel_hi:[1,0,1]
	v_pk_mul_f32 v[28:29], v[22:23], v[26:27] op_sel:[1,1] op_sel_hi:[1,0] neg_lo:[1,0]
	v_pk_fma_f32 v[22:23], v[22:23], v[26:27], v[28:29] op_sel_hi:[0,1,1]
	v_pk_mul_f32 v[28:29], v[16:17], v[26:27] op_sel:[1,1] op_sel_hi:[0,1] neg_lo:[0,1]
	v_pk_fma_f32 v[26:27], v[16:17], v[26:27], v[28:29] op_sel_hi:[1,0,1]
	v_pk_mul_f32 v[28:29], v[40:41], v[26:27] op_sel:[1,1] op_sel_hi:[1,0] neg_lo:[1,0]
	v_pk_fma_f32 v[28:29], v[40:41], v[26:27], v[28:29] op_sel_hi:[0,1,1]
	ds_write2_b64 v63, v[22:23], v[28:29] offset0:128 offset1:144
	v_pk_mul_f32 v[22:23], v[16:17], v[26:27] op_sel:[1,1] op_sel_hi:[0,1] neg_lo:[0,1]
	v_pk_fma_f32 v[22:23], v[16:17], v[26:27], v[22:23] op_sel_hi:[1,0,1]
	v_pk_mul_f32 v[26:27], v[24:25], v[22:23] op_sel:[1,1] op_sel_hi:[1,0] neg_lo:[1,0]
	v_pk_fma_f32 v[24:25], v[24:25], v[22:23], v[26:27] op_sel_hi:[0,1,1]
	v_pk_mul_f32 v[26:27], v[16:17], v[22:23] op_sel:[1,1] op_sel_hi:[0,1] neg_lo:[0,1]
	v_pk_fma_f32 v[22:23], v[16:17], v[22:23], v[26:27] op_sel_hi:[1,0,1]
	v_pk_mul_f32 v[26:27], v[44:45], v[22:23] op_sel:[1,1] op_sel_hi:[1,0] neg_lo:[1,0]
	v_pk_fma_f32 v[26:27], v[44:45], v[22:23], v[26:27] op_sel_hi:[0,1,1]
	ds_write2_b64 v62, v[24:25], v[26:27] offset0:160 offset1:176
	v_pk_mul_f32 v[24:25], v[16:17], v[22:23] op_sel:[1,1] op_sel_hi:[0,1] neg_lo:[0,1]
	v_pk_fma_f32 v[22:23], v[16:17], v[22:23], v[24:25] op_sel_hi:[1,0,1]
	v_pk_mul_f32 v[24:25], v[18:19], v[22:23] op_sel:[1,1] op_sel_hi:[1,0] neg_lo:[1,0]
	v_pk_fma_f32 v[18:19], v[18:19], v[22:23], v[24:25] op_sel_hi:[0,1,1]
	v_pk_mul_f32 v[24:25], v[16:17], v[22:23] op_sel:[1,1] op_sel_hi:[0,1] neg_lo:[0,1]
	v_pk_fma_f32 v[22:23], v[16:17], v[22:23], v[24:25] op_sel_hi:[1,0,1]
	v_pk_mul_f32 v[24:25], v[32:33], v[22:23] op_sel:[1,1] op_sel_hi:[1,0] neg_lo:[1,0]
	v_pk_fma_f32 v[24:25], v[32:33], v[22:23], v[24:25] op_sel_hi:[0,1,1]
	ds_write2_b64 v15, v[18:19], v[24:25] offset0:192 offset1:208
	v_pk_mul_f32 v[18:19], v[16:17], v[22:23] op_sel:[1,1] op_sel_hi:[0,1] neg_lo:[0,1]
	v_pk_fma_f32 v[18:19], v[16:17], v[22:23], v[18:19] op_sel_hi:[1,0,1]
	v_pk_mul_f32 v[22:23], v[20:21], v[18:19] op_sel:[1,1] op_sel_hi:[1,0] neg_lo:[1,0]
	v_pk_fma_f32 v[20:21], v[20:21], v[18:19], v[22:23] op_sel_hi:[0,1,1]
	v_pk_mul_f32 v[22:23], v[16:17], v[18:19] op_sel:[1,1] op_sel_hi:[0,1] neg_lo:[0,1]
	v_pk_fma_f32 v[16:17], v[16:17], v[18:19], v[22:23] op_sel_hi:[1,0,1]
	v_pk_mul_f32 v[18:19], v[36:37], v[16:17] op_sel:[1,1] op_sel_hi:[1,0] neg_lo:[1,0]
	v_pk_fma_f32 v[16:17], v[36:37], v[16:17], v[18:19] op_sel_hi:[0,1,1]
	ds_write2_b64 v13, v[20:21], v[16:17] offset0:224 offset1:240
	v_mov_b32_e32 v16, v1
	v_mov_b32_e32 v10, v178
	v_mov_b32_e32 v17, v177
	s_waitcnt lgkmcnt(0)
	s_barrier
	v_lshlrev_b32_e32 v190, 3, v16
	v_add_u32_e32 v190, 0x1000, v190
	global_load_dwordx2 v[196:197], v190, s[48:49] offset:-4096
	global_load_dwordx2 v[198:199], v190, s[48:49]
	v_add_u32_e32 v190, 0x2000, v190
	global_load_dwordx2 v[200:201], v190, s[48:49] offset:-4096
	global_load_dwordx2 v[202:203], v190, s[48:49]
	v_add_u32_e32 v190, 0x2000, v190
	global_load_dwordx2 v[204:205], v190, s[48:49] offset:-4096
	global_load_dwordx2 v[206:207], v190, s[48:49]
	v_add_u32_e32 v190, 0x2000, v190
	global_load_dwordx2 v[208:209], v190, s[48:49] offset:-4096
	global_load_dwordx2 v[210:211], v190, s[48:49]
	v_add_u32_e32 v190, 0x2000, v190
	global_load_dwordx2 v[212:213], v190, s[48:49] offset:-4096
	global_load_dwordx2 v[214:215], v190, s[48:49]
	v_add_u32_e32 v190, 0x2000, v190
	global_load_dwordx2 v[216:217], v190, s[48:49] offset:-4096
	global_load_dwordx2 v[218:219], v190, s[48:49]
	v_add_u32_e32 v190, 0x2000, v190
	global_load_dwordx2 v[220:221], v190, s[48:49] offset:-4096
	global_load_dwordx2 v[222:223], v190, s[48:49]
	v_add_u32_e32 v190, 0x2000, v190
	global_load_dwordx2 v[224:225], v190, s[48:49] offset:-4096
	global_load_dwordx2 v[226:227], v190, s[48:49]
	v_mov_b32_e32 v50, v166
	v_lshlrev_b32_e32 v13, 3, v17
	v_lshlrev_b32_e32 v48, 3, v10
	v_add3_u32 v10, 0, v13, v48
	v_xor_b32_e32 v13, 1, v17
	v_xor_b32_e32 v34, 8, v17
	v_xor_b32_e32 v36, 9, v17
	v_lshlrev_b32_e32 v13, 3, v13
	v_xor_b32_e32 v15, 2, v17
	v_xor_b32_e32 v24, 3, v17
	v_xor_b32_e32 v26, 4, v17
	v_xor_b32_e32 v28, 5, v17
	v_xor_b32_e32 v30, 6, v17
	v_xor_b32_e32 v32, 7, v17
	v_lshlrev_b32_e32 v34, 3, v34
	v_lshlrev_b32_e32 v36, 3, v36
	v_xor_b32_e32 v38, 10, v17
	v_xor_b32_e32 v40, 11, v17
	v_xor_b32_e32 v42, 12, v17
	v_xor_b32_e32 v44, 13, v17
	v_xor_b32_e32 v46, 14, v17
	v_xor_b32_e32 v17, 15, v17
	v_add3_u32 v13, 0, v13, v48
	v_lshlrev_b32_e32 v15, 3, v15
	v_lshlrev_b32_e32 v24, 3, v24
	v_lshlrev_b32_e32 v26, 3, v26
	v_lshlrev_b32_e32 v28, 3, v28
	v_lshlrev_b32_e32 v30, 3, v30
	v_lshlrev_b32_e32 v32, 3, v32
	v_add3_u32 v57, 0, v34, v48
	v_add3_u32 v58, 0, v36, v48
	v_lshlrev_b32_e32 v38, 3, v38
	v_lshlrev_b32_e32 v40, 3, v40
	v_lshlrev_b32_e32 v42, 3, v42
	v_lshlrev_b32_e32 v44, 3, v44
	v_lshlrev_b32_e32 v46, 3, v46
	v_lshlrev_b32_e32 v17, 3, v17
	ds_read_b64 v[18:19], v10
	ds_read_b64 v[20:21], v13
	v_add3_u32 v15, 0, v15, v48
	v_add3_u32 v52, 0, v24, v48
	v_add3_u32 v53, 0, v26, v48
	v_add3_u32 v54, 0, v28, v48
	v_add3_u32 v55, 0, v30, v48
	v_add3_u32 v56, 0, v32, v48
	ds_read_b64 v[34:35], v57
	ds_read_b64 v[36:37], v58
	v_add3_u32 v59, 0, v38, v48
	v_add3_u32 v60, 0, v40, v48
	v_add3_u32 v61, 0, v42, v48
	v_add3_u32 v62, 0, v44, v48
	v_add3_u32 v63, 0, v46, v48
	v_add3_u32 v64, 0, v17, v48
	v_mov_b32_e32 v17, v164
	ds_read_b64 v[22:23], v15
	ds_read_b64 v[24:25], v52
	ds_read_b64 v[26:27], v53
	ds_read_b64 v[28:29], v54
	ds_read_b64 v[30:31], v55
	ds_read_b64 v[32:33], v56
	ds_read_b64 v[38:39], v59
	ds_read_b64 v[40:41], v60
	ds_read_b64 v[42:43], v61
	ds_read_b64 v[44:45], v62
	ds_read_b64 v[46:47], v63
	ds_read_b64 v[48:49], v64
	s_waitcnt lgkmcnt(13)
	v_pk_add_f32 v[70:71], v[18:19], v[34:35]
	v_mov_b32_e32 v17, v165
	v_pk_add_f32 v[18:19], v[18:19], v[34:35] neg_lo:[0,1] neg_hi:[0,1]
	v_mov_b32_e32 v17, v167
	s_waitcnt lgkmcnt(12)
	v_pk_add_f32 v[34:35], v[20:21], v[36:37]
	v_pk_add_f32 v[20:21], v[20:21], v[36:37] neg_lo:[0,1] neg_hi:[0,1]
	v_mov_b32_e32 v66, v168
	v_mov_b32_e32 v17, v169
	v_mov_b32_e32 v68, v170
	s_nop 0
	v_pk_mul_f32 v[36:37], v[20:21], v[68:69] op_sel:[1,0] op_sel_hi:[0,0] neg_lo:[1,1] neg_hi:[0,1]
	v_mov_b32_e32 v17, v171
	v_pk_fma_f32 v[20:21], v[20:21], v[50:51], v[36:37] op_sel_hi:[1,0,1]
	s_waitcnt lgkmcnt(5)
	v_pk_add_f32 v[36:37], v[22:23], v[38:39]
	v_pk_add_f32 v[22:23], v[22:23], v[38:39] neg_lo:[0,1] neg_hi:[0,1]
	v_pk_mul_f32 v[38:39], v[22:23], v[66:67] op_sel:[1,0] op_sel_hi:[0,0] neg_lo:[1,1] neg_hi:[0,1]
	v_mov_b32_e32 v17, v172
	v_pk_fma_f32 v[22:23], v[22:23], v[66:67], v[38:39] op_sel_hi:[1,0,1]
	s_waitcnt lgkmcnt(4)
	v_pk_add_f32 v[38:39], v[24:25], v[40:41]
	v_pk_add_f32 v[24:25], v[24:25], v[40:41] neg_lo:[0,1] neg_hi:[0,1]
	v_pk_mul_f32 v[40:41], v[24:25], v[68:69] op_sel_hi:[1,0]
	v_pk_fma_f32 v[24:25], v[24:25], v[50:51], v[40:41] op_sel:[1,0,0] op_sel_hi:[0,0,1] neg_lo:[1,1,0] neg_hi:[0,1,0]
	s_waitcnt lgkmcnt(3)
	v_pk_add_f32 v[40:41], v[26:27], v[42:43]
	v_pk_add_f32 v[26:27], v[26:27], v[42:43] neg_lo:[0,1] neg_hi:[0,1]
	v_ashrrev_i32_e32 v17, 31, v16
	v_xor_b32_e32 v73, 0x80000000, v26
	v_mov_b32_e32 v72, v27
	s_waitcnt lgkmcnt(2)
	v_pk_add_f32 v[26:27], v[28:29], v[44:45]
	v_pk_add_f32 v[28:29], v[28:29], v[44:45] neg_lo:[0,1] neg_hi:[0,1]
	v_pk_mul_f32 v[42:43], v[28:29], v[68:69] op_sel_hi:[1,0] neg_lo:[0,1] neg_hi:[0,1]
	v_pk_fma_f32 v[28:29], v[28:29], v[50:51], v[42:43] op_sel:[1,0,0] op_sel_hi:[0,0,1] neg_lo:[1,1,0] neg_hi:[0,1,0]
	s_waitcnt lgkmcnt(1)
	v_pk_add_f32 v[42:43], v[30:31], v[46:47]
	v_pk_add_f32 v[30:31], v[30:31], v[46:47] neg_lo:[0,1] neg_hi:[0,1]
	v_pk_mul_f32 v[44:45], v[30:31], v[66:67] op_sel:[1,0] op_sel_hi:[0,0] neg_lo:[1,1] neg_hi:[0,1]
	v_pk_fma_f32 v[30:31], v[30:31], v[66:67], v[44:45] op_sel_hi:[1,0,1] neg_lo:[0,1,0] neg_hi:[0,1,0]
	s_waitcnt lgkmcnt(0)
	v_pk_add_f32 v[44:45], v[32:33], v[48:49]
	v_pk_add_f32 v[32:33], v[32:33], v[48:49] neg_lo:[0,1] neg_hi:[0,1]
	v_pk_add_f32 v[48:49], v[34:35], v[26:27]
	v_pk_add_f32 v[26:27], v[34:35], v[26:27] neg_lo:[0,1] neg_hi:[0,1]
	v_pk_mul_f32 v[34:35], v[26:27], v[66:67] op_sel:[1,0] op_sel_hi:[0,0] neg_lo:[1,1] neg_hi:[0,1]
	v_pk_fma_f32 v[26:27], v[26:27], v[66:67], v[34:35] op_sel_hi:[1,0,1]
	v_pk_add_f32 v[34:35], v[36:37], v[42:43]
	v_pk_add_f32 v[36:37], v[36:37], v[42:43] neg_lo:[0,1] neg_hi:[0,1]
	v_pk_mul_f32 v[46:47], v[32:33], v[68:69] op_sel:[1,0] op_sel_hi:[0,0] neg_lo:[1,1] neg_hi:[0,1]
	v_xor_b32_e32 v43, 0x80000000, v36
	v_mov_b32_e32 v42, v37
	v_pk_add_f32 v[36:37], v[38:39], v[44:45]
	v_pk_add_f32 v[38:39], v[38:39], v[44:45] neg_lo:[0,1] neg_hi:[0,1]
	v_pk_fma_f32 v[46:47], v[32:33], v[50:51], v[46:47] op_sel_hi:[1,0,1] neg_lo:[0,1,0] neg_hi:[0,1,0]
	v_pk_add_f32 v[32:33], v[70:71], v[40:41]
	v_pk_mul_f32 v[44:45], v[38:39], v[66:67] op_sel:[1,0] op_sel_hi:[0,0] neg_lo:[1,1] neg_hi:[0,1]
	v_pk_add_f32 v[40:41], v[70:71], v[40:41] neg_lo:[0,1] neg_hi:[0,1]
	v_pk_fma_f32 v[38:39], v[38:39], v[66:67], v[44:45] op_sel_hi:[1,0,1] neg_lo:[0,1,0] neg_hi:[0,1,0]
	v_pk_add_f32 v[44:45], v[32:33], v[34:35]
	v_pk_add_f32 v[32:33], v[32:33], v[34:35] neg_lo:[0,1] neg_hi:[0,1]
	v_pk_add_f32 v[34:35], v[48:49], v[36:37]
	v_pk_add_f32 v[36:37], v[48:49], v[36:37] neg_lo:[0,1] neg_hi:[0,1]
	v_pk_add_f32 v[50:51], v[44:45], v[34:35]
	v_xor_b32_e32 v49, 0x80000000, v36
	v_mov_b32_e32 v48, v37
	v_pk_add_f32 v[36:37], v[44:45], v[34:35] neg_lo:[0,1] neg_hi:[0,1]
	v_pk_add_f32 v[68:69], v[32:33], v[48:49]
	v_pk_add_f32 v[44:45], v[32:33], v[48:49] neg_lo:[0,1] neg_hi:[0,1]
	v_pk_add_f32 v[32:33], v[40:41], v[42:43]
	v_pk_add_f32 v[34:35], v[40:41], v[42:43] neg_lo:[0,1] neg_hi:[0,1]
	v_pk_add_f32 v[40:41], v[26:27], v[38:39]
	v_pk_add_f32 v[26:27], v[26:27], v[38:39] neg_lo:[0,1] neg_hi:[0,1]
	v_pk_add_f32 v[42:43], v[32:33], v[40:41] neg_lo:[0,1] neg_hi:[0,1]
	v_xor_b32_e32 v39, 0x80000000, v26
	v_mov_b32_e32 v38, v27
	v_pk_add_f32 v[26:27], v[32:33], v[40:41]
	v_pk_add_f32 v[40:41], v[20:21], v[28:29]
	v_pk_add_f32 v[20:21], v[20:21], v[28:29] neg_lo:[0,1] neg_hi:[0,1]
	v_pk_add_f32 v[32:33], v[34:35], v[38:39]
	v_pk_mul_f32 v[28:29], v[66:67], v[20:21] op_sel:[0,1] op_sel_hi:[0,0] neg_lo:[1,1] neg_hi:[1,0]
	v_pk_fma_f32 v[20:21], v[66:67], v[20:21], v[28:29] op_sel_hi:[0,1,1]
	v_pk_add_f32 v[28:29], v[22:23], v[30:31]
	v_pk_add_f32 v[22:23], v[22:23], v[30:31] neg_lo:[0,1] neg_hi:[0,1]
	v_pk_add_f32 v[38:39], v[34:35], v[38:39] neg_lo:[0,1] neg_hi:[0,1]
	v_xor_b32_e32 v31, 0x80000000, v22
	v_mov_b32_e32 v30, v23
	v_pk_add_f32 v[22:23], v[24:25], v[46:47]
	v_pk_add_f32 v[24:25], v[24:25], v[46:47] neg_lo:[0,1] neg_hi:[0,1]
	v_pk_add_f32 v[34:35], v[18:19], v[72:73]
	v_pk_mul_f32 v[46:47], v[66:67], v[24:25] op_sel:[0,1] op_sel_hi:[0,0] neg_lo:[1,1] neg_hi:[1,0]
	v_pk_fma_f32 v[24:25], v[66:67], v[24:25], v[46:47] op_sel_hi:[0,1,1] neg_lo:[1,0,0] neg_hi:[1,0,0]
	v_pk_add_f32 v[46:47], v[34:35], v[28:29]
	v_pk_add_f32 v[28:29], v[34:35], v[28:29] neg_lo:[0,1] neg_hi:[0,1]
	v_pk_add_f32 v[34:35], v[40:41], v[22:23]
	v_pk_add_f32 v[22:23], v[40:41], v[22:23] neg_lo:[0,1] neg_hi:[0,1]
	v_pk_add_f32 v[18:19], v[18:19], v[72:73] neg_lo:[0,1] neg_hi:[0,1]
	v_pk_add_f32 v[66:67], v[28:29], v[22:23] op_sel:[0,1] op_sel_hi:[1,0] neg_hi:[0,1]
	v_pk_add_f32 v[48:49], v[28:29], v[22:23] op_sel:[0,1] op_sel_hi:[1,0] neg_lo:[0,1]
	v_pk_add_f32 v[28:29], v[18:19], v[30:31]
	v_pk_add_f32 v[18:19], v[18:19], v[30:31] neg_lo:[0,1] neg_hi:[0,1]
	v_pk_add_f32 v[30:31], v[20:21], v[24:25]
	v_pk_add_f32 v[20:21], v[20:21], v[24:25] neg_lo:[0,1] neg_hi:[0,1]
	v_pk_add_f32 v[22:23], v[46:47], v[34:35]
	v_xor_b32_e32 v25, 0x80000000, v20
	v_mov_b32_e32 v24, v21
	v_lshl_add_u64 v[20:21], v[16:17], 3, s[48:49]
	s_waitcnt vmcnt(0)
	v_pk_add_f32 v[40:41], v[46:47], v[34:35] neg_lo:[0,1] neg_hi:[0,1]
	v_pk_add_f32 v[34:35], v[18:19], v[24:25]
	v_pk_add_f32 v[18:19], v[18:19], v[24:25] neg_lo:[0,1] neg_hi:[0,1]
	v_pk_add_f32 v[70:71], v[28:29], v[30:31]
	v_pk_add_f32 v[46:47], v[28:29], v[30:31] neg_lo:[0,1] neg_hi:[0,1]
	v_mov_b32_e32 v17, v164
	s_nop 0
	v_pk_mul_f32 v[24:25], v[50:51], v[196:197] op_sel:[1,1] op_sel_hi:[1,0] neg_lo:[1,0]
	v_pk_fma_f32 v[20:21], v[50:51], v[196:197], v[24:25] op_sel_hi:[0,1,1]
	v_add_u32_e32 v24, 0x200, v16
	v_ashrrev_i32_e32 v25, 31, v24
	v_lshl_add_u64 v[24:25], v[24:25], 3, s[48:49]
	s_nop 0
	v_pk_mul_f32 v[28:29], v[198:199], v[22:23] op_sel:[1,1] op_sel_hi:[0,1] neg_lo:[0,1]
	v_pk_fma_f32 v[22:23], v[198:199], v[22:23], v[28:29] op_sel_hi:[1,0,1]
	v_add_u32_e32 v24, 0x400, v16
	v_ashrrev_i32_e32 v25, 31, v24
	v_lshl_add_u64 v[24:25], v[24:25], 3, s[48:49]
	s_nop 0
	v_pk_mul_f32 v[28:29], v[26:27], v[200:201] op_sel:[1,1] op_sel_hi:[1,0] neg_lo:[1,0]
	v_pk_fma_f32 v[24:25], v[26:27], v[200:201], v[28:29] op_sel_hi:[0,1,1]
	v_add_u32_e32 v26, 0x600, v16
	v_ashrrev_i32_e32 v27, 31, v26
	v_lshl_add_u64 v[26:27], v[26:27], 3, s[48:49]
	s_nop 0
	v_pk_mul_f32 v[28:29], v[202:203], v[70:71] op_sel:[1,1] op_sel_hi:[0,1] neg_lo:[0,1]
	v_pk_fma_f32 v[26:27], v[202:203], v[70:71], v[28:29] op_sel_hi:[1,0,1]
	v_add_u32_e32 v28, 0x800, v16
	v_ashrrev_i32_e32 v29, 31, v28
	v_lshl_add_u64 v[28:29], v[28:29], 3, s[48:49]
	s_nop 0
	v_pk_mul_f32 v[30:31], v[68:69], v[204:205] op_sel:[1,1] op_sel_hi:[1,0] neg_lo:[1,0]
	v_pk_fma_f32 v[28:29], v[68:69], v[204:205], v[30:31] op_sel_hi:[0,1,1]
	v_add_u32_e32 v30, 0xa00, v16
	v_ashrrev_i32_e32 v31, 31, v30
	v_lshl_add_u64 v[30:31], v[30:31], 3, s[48:49]
	v_mov_b32_e32 v68, v170
	s_nop 0
	v_pk_mul_f32 v[50:51], v[206:207], v[66:67] op_sel:[1,1] op_sel_hi:[0,1] neg_lo:[0,1]
	v_pk_fma_f32 v[30:31], v[206:207], v[66:67], v[50:51] op_sel_hi:[1,0,1]
	v_add_u32_e32 v50, 0xc00, v16
	v_ashrrev_i32_e32 v51, 31, v50
	v_lshl_add_u64 v[50:51], v[50:51], 3, s[48:49]
	s_nop 0
	v_pk_mul_f32 v[66:67], v[32:33], v[208:209] op_sel:[1,1] op_sel_hi:[1,0] neg_lo:[1,0]
	v_pk_fma_f32 v[32:33], v[32:33], v[208:209], v[66:67] op_sel_hi:[0,1,1]
	v_add_u32_e32 v50, 0xe00, v16
	v_ashrrev_i32_e32 v51, 31, v50
	v_lshl_add_u64 v[50:51], v[50:51], 3, s[48:49]
	s_nop 0
	v_pk_mul_f32 v[66:67], v[210:211], v[34:35] op_sel:[1,1] op_sel_hi:[0,1] neg_lo:[0,1]
	v_pk_fma_f32 v[34:35], v[210:211], v[34:35], v[66:67] op_sel_hi:[1,0,1]
	v_add_u32_e32 v50, 0x1000, v16
	v_ashrrev_i32_e32 v51, 31, v50
	v_lshl_add_u64 v[50:51], v[50:51], 3, s[48:49]
	s_nop 0
	v_pk_mul_f32 v[66:67], v[36:37], v[212:213] op_sel:[1,1] op_sel_hi:[1,0] neg_lo:[1,0]
	v_pk_fma_f32 v[36:37], v[36:37], v[212:213], v[66:67] op_sel_hi:[0,1,1]
	v_add_u32_e32 v50, 0x1200, v16
	v_ashrrev_i32_e32 v51, 31, v50
	v_lshl_add_u64 v[50:51], v[50:51], 3, s[48:49]
	v_pk_add_f32 v[70:71], v[20:21], v[36:37]
	v_pk_add_f32 v[20:21], v[20:21], v[36:37] neg_lo:[0,1] neg_hi:[0,1]
	s_nop 0
	v_pk_mul_f32 v[66:67], v[40:41], v[214:215] op_sel:[1,1] op_sel_hi:[1,0] neg_lo:[1,0]
	v_pk_fma_f32 v[40:41], v[40:41], v[214:215], v[66:67] op_sel_hi:[0,1,1]
	v_add_u32_e32 v50, 0x1400, v16
	v_ashrrev_i32_e32 v51, 31, v50
	v_lshl_add_u64 v[50:51], v[50:51], 3, s[48:49]
	v_pk_add_f32 v[36:37], v[22:23], v[40:41]
	v_pk_add_f32 v[22:23], v[22:23], v[40:41] neg_lo:[0,1] neg_hi:[0,1]
	s_nop 0
	v_pk_mul_f32 v[66:67], v[42:43], v[216:217] op_sel:[1,1] op_sel_hi:[1,0] neg_lo:[1,0]
	v_pk_fma_f32 v[42:43], v[42:43], v[216:217], v[66:67] op_sel_hi:[0,1,1]
	v_add_u32_e32 v50, 0x1600, v16
	v_ashrrev_i32_e32 v51, 31, v50
	v_lshl_add_u64 v[50:51], v[50:51], 3, s[48:49]
	s_nop 0
	v_pk_mul_f32 v[66:67], v[46:47], v[218:219] op_sel:[1,1] op_sel_hi:[1,0] neg_lo:[1,0]
	v_pk_fma_f32 v[46:47], v[46:47], v[218:219], v[66:67] op_sel_hi:[0,1,1]
	v_add_u32_e32 v50, 0x1800, v16
	v_ashrrev_i32_e32 v51, 31, v50
	v_lshl_add_u64 v[50:51], v[50:51], 3, s[48:49]
	s_nop 0
	v_pk_mul_f32 v[66:67], v[44:45], v[220:221] op_sel:[1,1] op_sel_hi:[1,0] neg_lo:[1,0]
	v_pk_fma_f32 v[44:45], v[44:45], v[220:221], v[66:67] op_sel_hi:[0,1,1]
	v_add_u32_e32 v50, 0x1a00, v16
	v_ashrrev_i32_e32 v51, 31, v50
	v_lshl_add_u64 v[50:51], v[50:51], 3, s[48:49]
	s_nop 0
	v_pk_mul_f32 v[66:67], v[48:49], v[222:223] op_sel:[1,1] op_sel_hi:[1,0] neg_lo:[1,0]
	v_pk_fma_f32 v[48:49], v[48:49], v[222:223], v[66:67] op_sel_hi:[0,1,1]
	v_add_u32_e32 v50, 0x1c00, v16
	v_ashrrev_i32_e32 v51, 31, v50
	v_lshl_add_u64 v[50:51], v[50:51], 3, s[48:49]
	s_nop 0
	v_pk_mul_f32 v[66:67], v[38:39], v[224:225] op_sel:[1,1] op_sel_hi:[1,0] neg_lo:[1,0]
	v_pk_fma_f32 v[38:39], v[38:39], v[224:225], v[66:67] op_sel_hi:[0,1,1]
	v_add_u32_e32 v50, 0x1e00, v16
	v_ashrrev_i32_e32 v51, 31, v50
	v_lshl_add_u64 v[50:51], v[50:51], 3, s[48:49]
	v_mov_b32_e32 v50, v226
	v_mov_b32_e32 v51, v227
	v_lshlrev_b32_e32 v190, 3, v16
	v_add_u32_e32 v190, 0x11000, v190
	global_load_dwordx2 v[196:197], v190, s[48:49] offset:-4096
	global_load_dwordx2 v[198:199], v190, s[48:49]
	v_add_u32_e32 v190, 0x2000, v190
	global_load_dwordx2 v[200:201], v190, s[48:49] offset:-4096
	global_load_dwordx2 v[202:203], v190, s[48:49]
	v_add_u32_e32 v190, 0x2000, v190
	global_load_dwordx2 v[204:205], v190, s[48:49] offset:-4096
	global_load_dwordx2 v[206:207], v190, s[48:49]
	v_add_u32_e32 v190, 0x2000, v190
	global_load_dwordx2 v[208:209], v190, s[48:49] offset:-4096
	global_load_dwordx2 v[210:211], v190, s[48:49]
	v_add_u32_e32 v190, 0x2000, v190
	global_load_dwordx2 v[212:213], v190, s[48:49] offset:-4096
	global_load_dwordx2 v[214:215], v190, s[48:49]
	v_add_u32_e32 v190, 0x2000, v190
	global_load_dwordx2 v[216:217], v190, s[48:49] offset:-4096
	global_load_dwordx2 v[218:219], v190, s[48:49]
	v_add_u32_e32 v190, 0x2000, v190
	global_load_dwordx2 v[220:221], v190, s[48:49] offset:-4096
	global_load_dwordx2 v[222:223], v190, s[48:49]
	v_add_u32_e32 v190, 0x2000, v190
	global_load_dwordx2 v[224:225], v190, s[48:49] offset:-4096
	global_load_dwordx2 v[226:227], v190, s[48:49]
	v_mov_b32_e32 v17, v165
	s_nop 0
	v_pk_mul_f32 v[66:67], v[18:19], v[50:51] op_sel:[1,1] op_sel_hi:[1,0] neg_lo:[1,0]
	v_pk_fma_f32 v[18:19], v[18:19], v[50:51], v[66:67] op_sel_hi:[0,1,1]
	v_mov_b32_e32 v50, v166
	v_mov_b32_e32 v17, v167
	v_mov_b32_e32 v66, v168
	v_mov_b32_e32 v17, v169
	s_nop 0
	v_pk_mul_f32 v[40:41], v[22:23], v[68:69] op_sel:[1,0] op_sel_hi:[0,0] neg_lo:[1,0]
	v_mov_b32_e32 v17, v171
	v_pk_fma_f32 v[22:23], v[22:23], v[50:51], v[40:41] op_sel_hi:[1,0,1]
	v_pk_add_f32 v[40:41], v[24:25], v[42:43]
	v_pk_add_f32 v[24:25], v[24:25], v[42:43] neg_lo:[0,1] neg_hi:[0,1]
	v_pk_mul_f32 v[42:43], v[24:25], v[66:67] op_sel:[1,0] op_sel_hi:[0,0] neg_lo:[1,0]
	v_mov_b32_e32 v17, v172
	v_pk_fma_f32 v[24:25], v[24:25], v[66:67], v[42:43] op_sel_hi:[1,0,1]
	v_pk_add_f32 v[42:43], v[26:27], v[46:47]
	v_pk_add_f32 v[26:27], v[26:27], v[46:47] neg_lo:[0,1] neg_hi:[0,1]
	v_pk_mul_f32 v[46:47], v[26:27], v[68:69] op_sel_hi:[1,0]
	v_pk_fma_f32 v[26:27], v[26:27], v[50:51], v[46:47] op_sel:[1,0,0] op_sel_hi:[0,0,1] neg_lo:[1,0,0]
	v_pk_add_f32 v[46:47], v[28:29], v[44:45]
	v_pk_add_f32 v[28:29], v[28:29], v[44:45] neg_lo:[0,1] neg_hi:[0,1]
	v_mov_b32_e32 v17, v177
	v_xor_b32_e32 v44, 0x80000000, v29
	v_mov_b32_e32 v45, v28
	v_pk_add_f32 v[28:29], v[30:31], v[48:49]
	v_pk_add_f32 v[30:31], v[30:31], v[48:49] neg_lo:[0,1] neg_hi:[0,1]
	v_pk_mul_f32 v[48:49], v[30:31], v[68:69] op_sel_hi:[1,0] neg_lo:[0,1] neg_hi:[0,1]
	v_pk_fma_f32 v[30:31], v[30:31], v[50:51], v[48:49] op_sel:[1,0,0] op_sel_hi:[0,0,1] neg_lo:[1,0,0]
	v_pk_add_f32 v[48:49], v[32:33], v[38:39]
	v_pk_add_f32 v[32:33], v[32:33], v[38:39] neg_lo:[0,1] neg_hi:[0,1]
	v_pk_mul_f32 v[38:39], v[32:33], v[66:67] op_sel:[1,0] op_sel_hi:[0,0] neg_lo:[1,0]
	v_pk_fma_f32 v[32:33], v[32:33], v[66:67], v[38:39] op_sel_hi:[1,0,1] neg_lo:[0,1,0] neg_hi:[0,1,0]
	v_pk_add_f32 v[38:39], v[34:35], v[18:19]
	v_pk_add_f32 v[18:19], v[34:35], v[18:19] neg_lo:[0,1] neg_hi:[0,1]
	v_pk_mul_f32 v[34:35], v[18:19], v[68:69] op_sel:[1,0] op_sel_hi:[0,0] neg_lo:[1,0]
	v_mov_b32_e32 v68, v170
	v_pk_fma_f32 v[18:19], v[18:19], v[50:51], v[34:35] op_sel_hi:[1,0,1] neg_lo:[0,1,0] neg_hi:[0,1,0]
	v_pk_add_f32 v[50:51], v[36:37], v[28:29]
	v_pk_add_f32 v[28:29], v[36:37], v[28:29] neg_lo:[0,1] neg_hi:[0,1]
	v_pk_add_f32 v[34:35], v[70:71], v[46:47]
	v_pk_mul_f32 v[36:37], v[28:29], v[66:67] op_sel:[1,0] op_sel_hi:[0,0] neg_lo:[1,0]
	v_pk_add_f32 v[46:47], v[70:71], v[46:47] neg_lo:[0,1] neg_hi:[0,1]
	v_pk_fma_f32 v[28:29], v[28:29], v[66:67], v[36:37] op_sel_hi:[1,0,1]
	v_pk_add_f32 v[36:37], v[40:41], v[48:49]
	v_pk_add_f32 v[40:41], v[40:41], v[48:49] neg_lo:[0,1] neg_hi:[0,1]
	v_xor_b32_e32 v48, 0x80000000, v41
	v_mov_b32_e32 v49, v40
	v_pk_add_f32 v[40:41], v[42:43], v[38:39]
	v_pk_add_f32 v[38:39], v[42:43], v[38:39] neg_lo:[0,1] neg_hi:[0,1]
	v_pk_mul_f32 v[42:43], v[66:67], v[38:39] op_sel:[0,1] op_sel_hi:[0,0] neg_lo:[0,1]
	v_pk_fma_f32 v[38:39], v[38:39], v[66:67], v[42:43] op_sel_hi:[1,0,1] neg_lo:[0,1,0] neg_hi:[0,1,0]
	v_pk_add_f32 v[42:43], v[34:35], v[36:37]
	v_pk_add_f32 v[34:35], v[34:35], v[36:37] neg_lo:[0,1] neg_hi:[0,1]
	v_pk_add_f32 v[36:37], v[50:51], v[40:41]
	v_pk_add_f32 v[40:41], v[50:51], v[40:41] neg_lo:[0,1] neg_hi:[0,1]
	v_xor_b32_e32 v50, 0x80000000, v41
	v_mov_b32_e32 v51, v40
	v_pk_add_f32 v[40:41], v[42:43], v[36:37]
	v_pk_add_f32 v[36:37], v[42:43], v[36:37] neg_lo:[0,1] neg_hi:[0,1]
	v_pk_add_f32 v[42:43], v[34:35], v[50:51]
	v_pk_add_f32 v[34:35], v[34:35], v[50:51] neg_lo:[0,1] neg_hi:[0,1]
	v_pk_add_f32 v[50:51], v[46:47], v[48:49]
	v_pk_add_f32 v[46:47], v[46:47], v[48:49] neg_lo:[0,1] neg_hi:[0,1]
	v_pk_add_f32 v[48:49], v[28:29], v[38:39]
	v_pk_add_f32 v[28:29], v[28:29], v[38:39] neg_lo:[0,1] neg_hi:[0,1]
	v_xor_b32_e32 v38, 0x80000000, v29
	v_mov_b32_e32 v39, v28
	v_pk_add_f32 v[28:29], v[50:51], v[48:49]
	v_pk_add_f32 v[48:49], v[50:51], v[48:49] neg_lo:[0,1] neg_hi:[0,1]
	v_pk_add_f32 v[50:51], v[46:47], v[38:39]
	v_pk_add_f32 v[38:39], v[46:47], v[38:39] neg_lo:[0,1] neg_hi:[0,1]
	v_pk_add_f32 v[46:47], v[20:21], v[44:45]
	v_pk_add_f32 v[20:21], v[20:21], v[44:45] neg_lo:[0,1] neg_hi:[0,1]
	v_pk_add_f32 v[44:45], v[22:23], v[30:31]
	v_pk_add_f32 v[22:23], v[22:23], v[30:31] neg_lo:[0,1] neg_hi:[0,1]
	v_pk_mul_f32 v[30:31], v[66:67], v[22:23] op_sel:[0,1] op_sel_hi:[0,0] neg_lo:[0,1]
	v_pk_fma_f32 v[22:23], v[66:67], v[22:23], v[30:31] op_sel_hi:[0,1,1]
	v_pk_add_f32 v[30:31], v[24:25], v[32:33]
	v_pk_add_f32 v[24:25], v[24:25], v[32:33] neg_lo:[0,1] neg_hi:[0,1]
	v_xor_b32_e32 v32, 0x80000000, v25
	v_mov_b32_e32 v33, v24
	v_pk_add_f32 v[24:25], v[26:27], v[18:19]
	v_pk_add_f32 v[18:19], v[26:27], v[18:19] neg_lo:[0,1] neg_hi:[0,1]
	v_pk_mul_f32 v[26:27], v[66:67], v[18:19] op_sel:[0,1] op_sel_hi:[0,0] neg_lo:[0,1]
	v_pk_fma_f32 v[18:19], v[66:67], v[18:19], v[26:27] op_sel_hi:[0,1,1] neg_lo:[1,0,0] neg_hi:[1,0,0]
	v_pk_add_f32 v[26:27], v[46:47], v[30:31]
	v_pk_add_f32 v[30:31], v[46:47], v[30:31] neg_lo:[0,1] neg_hi:[0,1]
	v_pk_add_f32 v[46:47], v[44:45], v[24:25]
	v_pk_add_f32 v[24:25], v[44:45], v[24:25] neg_lo:[0,1] neg_hi:[0,1]
	v_mov_b32_e32 v66, v168
	v_xor_b32_e32 v44, 0x80000000, v25
	v_mov_b32_e32 v45, v24
	v_pk_add_f32 v[24:25], v[26:27], v[46:47]
	v_pk_add_f32 v[26:27], v[26:27], v[46:47] neg_lo:[0,1] neg_hi:[0,1]
	v_pk_add_f32 v[46:47], v[30:31], v[44:45]
	v_pk_add_f32 v[30:31], v[30:31], v[44:45] neg_lo:[0,1] neg_hi:[0,1]
	v_pk_add_f32 v[44:45], v[20:21], v[32:33]
	v_pk_add_f32 v[20:21], v[20:21], v[32:33] neg_lo:[0,1] neg_hi:[0,1]
	v_pk_add_f32 v[32:33], v[22:23], v[18:19]
	v_pk_add_f32 v[18:19], v[22:23], v[18:19] neg_lo:[0,1] neg_hi:[0,1]
	v_xor_b32_e32 v22, 0x80000000, v19
	v_mov_b32_e32 v23, v18
	v_pk_add_f32 v[18:19], v[44:45], v[32:33]
	v_pk_add_f32 v[32:33], v[44:45], v[32:33] neg_lo:[0,1] neg_hi:[0,1]
	v_pk_add_f32 v[44:45], v[20:21], v[22:23]
	v_pk_add_f32 v[20:21], v[20:21], v[22:23] neg_lo:[0,1] neg_hi:[0,1]
	ds_write_b64 v10, v[40:41]
	ds_write_b64 v13, v[24:25]
	ds_write_b64 v15, v[28:29]
	ds_write_b64 v52, v[18:19]
	ds_write_b64 v53, v[42:43]
	ds_write_b64 v54, v[46:47]
	ds_write_b64 v55, v[50:51]
	ds_write_b64 v56, v[44:45]
	ds_write_b64 v57, v[36:37]
	ds_write_b64 v58, v[26:27]
	ds_write_b64 v59, v[48:49]
	ds_write_b64 v60, v[32:33]
	ds_write_b64 v61, v[34:35]
	ds_write_b64 v62, v[30:31]
	ds_write_b64 v63, v[38:39]
	ds_write_b64 v64, v[20:21]
	v_mov_b32_e32 v10, v179
	v_mov_b32_e32 v64, v166
	v_lshlrev_b32_e32 v13, 3, v17
	v_lshlrev_b32_e32 v48, 3, v10
	v_add3_u32 v10, 0, v13, v48
	v_xor_b32_e32 v13, 1, v17
	v_xor_b32_e32 v34, 8, v17
	v_xor_b32_e32 v36, 9, v17
	v_lshlrev_b32_e32 v13, 3, v13
	v_xor_b32_e32 v15, 2, v17
	v_xor_b32_e32 v24, 3, v17
	v_xor_b32_e32 v26, 4, v17
	v_xor_b32_e32 v28, 5, v17
	v_xor_b32_e32 v30, 6, v17
	v_xor_b32_e32 v32, 7, v17
	v_lshlrev_b32_e32 v34, 3, v34
	v_lshlrev_b32_e32 v36, 3, v36
	v_xor_b32_e32 v38, 10, v17
	v_xor_b32_e32 v40, 11, v17
	v_xor_b32_e32 v42, 12, v17
	v_xor_b32_e32 v44, 13, v17
	v_xor_b32_e32 v46, 14, v17
	v_xor_b32_e32 v17, 15, v17
	v_add3_u32 v13, 0, v13, v48
	v_lshlrev_b32_e32 v15, 3, v15
	v_lshlrev_b32_e32 v24, 3, v24
	v_lshlrev_b32_e32 v26, 3, v26
	v_lshlrev_b32_e32 v28, 3, v28
	v_lshlrev_b32_e32 v30, 3, v30
	v_lshlrev_b32_e32 v32, 3, v32
	v_add3_u32 v55, 0, v34, v48
	v_add3_u32 v56, 0, v36, v48
	v_lshlrev_b32_e32 v38, 3, v38
	v_lshlrev_b32_e32 v40, 3, v40
	v_lshlrev_b32_e32 v42, 3, v42
	v_lshlrev_b32_e32 v44, 3, v44
	v_lshlrev_b32_e32 v46, 3, v46
	v_lshlrev_b32_e32 v17, 3, v17
	ds_read_b64 v[18:19], v10
	ds_read_b64 v[20:21], v13
	v_add3_u32 v15, 0, v15, v48
	v_add3_u32 v50, 0, v24, v48
	v_add3_u32 v51, 0, v26, v48
	v_add3_u32 v52, 0, v28, v48
	v_add3_u32 v53, 0, v30, v48
	v_add3_u32 v54, 0, v32, v48
	ds_read_b64 v[34:35], v55
	ds_read_b64 v[36:37], v56
	v_add3_u32 v57, 0, v38, v48
	v_add3_u32 v58, 0, v40, v48
	v_add3_u32 v59, 0, v42, v48
	v_add3_u32 v60, 0, v44, v48
	v_add3_u32 v61, 0, v46, v48
	v_add3_u32 v62, 0, v17, v48
	v_mov_b32_e32 v17, v164
	ds_read_b64 v[22:23], v15
	ds_read_b64 v[24:25], v50
	ds_read_b64 v[26:27], v51
	ds_read_b64 v[28:29], v52
	ds_read_b64 v[30:31], v53
	ds_read_b64 v[32:33], v54
	ds_read_b64 v[38:39], v57
	ds_read_b64 v[40:41], v58
	ds_read_b64 v[42:43], v59
	ds_read_b64 v[44:45], v60
	ds_read_b64 v[46:47], v61
	ds_read_b64 v[48:49], v62
	s_waitcnt lgkmcnt(13)
	v_pk_add_f32 v[70:71], v[18:19], v[34:35]
	v_mov_b32_e32 v17, v165
	v_pk_add_f32 v[18:19], v[18:19], v[34:35] neg_lo:[0,1] neg_hi:[0,1]
	v_mov_b32_e32 v17, v167
	s_waitcnt lgkmcnt(12)
	v_pk_add_f32 v[34:35], v[20:21], v[36:37]
	v_pk_add_f32 v[20:21], v[20:21], v[36:37] neg_lo:[0,1] neg_hi:[0,1]
	v_mov_b32_e32 v17, v169
	s_nop 0
	v_pk_mul_f32 v[36:37], v[20:21], v[68:69] op_sel:[1,0] op_sel_hi:[0,0] neg_lo:[1,1] neg_hi:[0,1]
	v_mov_b32_e32 v17, v171
	v_pk_fma_f32 v[20:21], v[20:21], v[64:65], v[36:37] op_sel_hi:[1,0,1]
	s_waitcnt lgkmcnt(5)
	v_pk_add_f32 v[36:37], v[22:23], v[38:39]
	v_pk_add_f32 v[22:23], v[22:23], v[38:39] neg_lo:[0,1] neg_hi:[0,1]
	v_pk_mul_f32 v[38:39], v[22:23], v[66:67] op_sel:[1,0] op_sel_hi:[0,0] neg_lo:[1,1] neg_hi:[0,1]
	v_mov_b32_e32 v17, v172
	v_pk_fma_f32 v[22:23], v[22:23], v[66:67], v[38:39] op_sel_hi:[1,0,1]
	s_waitcnt lgkmcnt(4)
	v_pk_add_f32 v[38:39], v[24:25], v[40:41]
	v_pk_add_f32 v[24:25], v[24:25], v[40:41] neg_lo:[0,1] neg_hi:[0,1]
	v_pk_mul_f32 v[40:41], v[24:25], v[68:69] op_sel_hi:[1,0]
	v_pk_fma_f32 v[24:25], v[24:25], v[64:65], v[40:41] op_sel:[1,0,0] op_sel_hi:[0,0,1] neg_lo:[1,1,0] neg_hi:[0,1,0]
	s_waitcnt lgkmcnt(3)
	v_pk_add_f32 v[40:41], v[26:27], v[42:43]
	v_pk_add_f32 v[26:27], v[26:27], v[42:43] neg_lo:[0,1] neg_hi:[0,1]
	v_xor_b32_e32 v73, 0x80000000, v26
	v_mov_b32_e32 v72, v27
	s_waitcnt lgkmcnt(2)
	v_pk_add_f32 v[26:27], v[28:29], v[44:45]
	v_pk_add_f32 v[28:29], v[28:29], v[44:45] neg_lo:[0,1] neg_hi:[0,1]
	v_pk_mul_f32 v[42:43], v[28:29], v[68:69] op_sel_hi:[1,0] neg_lo:[0,1] neg_hi:[0,1]
	v_pk_fma_f32 v[28:29], v[28:29], v[64:65], v[42:43] op_sel:[1,0,0] op_sel_hi:[0,0,1] neg_lo:[1,1,0] neg_hi:[0,1,0]
	s_waitcnt lgkmcnt(1)
	v_pk_add_f32 v[42:43], v[30:31], v[46:47]
	v_pk_add_f32 v[30:31], v[30:31], v[46:47] neg_lo:[0,1] neg_hi:[0,1]
	v_pk_mul_f32 v[44:45], v[30:31], v[66:67] op_sel:[1,0] op_sel_hi:[0,0] neg_lo:[1,1] neg_hi:[0,1]
	v_pk_fma_f32 v[30:31], v[30:31], v[66:67], v[44:45] op_sel_hi:[1,0,1] neg_lo:[0,1,0] neg_hi:[0,1,0]
	s_waitcnt lgkmcnt(0)
	v_pk_add_f32 v[44:45], v[32:33], v[48:49]
	v_pk_add_f32 v[32:33], v[32:33], v[48:49] neg_lo:[0,1] neg_hi:[0,1]
	v_pk_add_f32 v[48:49], v[34:35], v[26:27]
	v_pk_add_f32 v[26:27], v[34:35], v[26:27] neg_lo:[0,1] neg_hi:[0,1]
	v_pk_mul_f32 v[34:35], v[26:27], v[66:67] op_sel:[1,0] op_sel_hi:[0,0] neg_lo:[1,1] neg_hi:[0,1]
	v_pk_fma_f32 v[26:27], v[26:27], v[66:67], v[34:35] op_sel_hi:[1,0,1]
	v_pk_add_f32 v[34:35], v[36:37], v[42:43]
	v_pk_add_f32 v[36:37], v[36:37], v[42:43] neg_lo:[0,1] neg_hi:[0,1]
	v_pk_mul_f32 v[46:47], v[32:33], v[68:69] op_sel:[1,0] op_sel_hi:[0,0] neg_lo:[1,1] neg_hi:[0,1]
	v_xor_b32_e32 v43, 0x80000000, v36
	v_mov_b32_e32 v42, v37
	v_pk_add_f32 v[36:37], v[38:39], v[44:45]
	v_pk_add_f32 v[38:39], v[38:39], v[44:45] neg_lo:[0,1] neg_hi:[0,1]
	v_pk_fma_f32 v[46:47], v[32:33], v[64:65], v[46:47] op_sel_hi:[1,0,1] neg_lo:[0,1,0] neg_hi:[0,1,0]
	v_pk_add_f32 v[32:33], v[70:71], v[40:41]
	v_pk_mul_f32 v[44:45], v[38:39], v[66:67] op_sel:[1,0] op_sel_hi:[0,0] neg_lo:[1,1] neg_hi:[0,1]
	v_pk_add_f32 v[40:41], v[70:71], v[40:41] neg_lo:[0,1] neg_hi:[0,1]
	v_pk_fma_f32 v[38:39], v[38:39], v[66:67], v[44:45] op_sel_hi:[1,0,1] neg_lo:[0,1,0] neg_hi:[0,1,0]
	v_pk_add_f32 v[44:45], v[32:33], v[34:35]
	v_pk_add_f32 v[32:33], v[32:33], v[34:35] neg_lo:[0,1] neg_hi:[0,1]
	v_pk_add_f32 v[34:35], v[48:49], v[36:37]
	v_pk_add_f32 v[36:37], v[48:49], v[36:37] neg_lo:[0,1] neg_hi:[0,1]
	v_pk_add_f32 v[64:65], v[44:45], v[34:35]
	v_xor_b32_e32 v49, 0x80000000, v36
	v_mov_b32_e32 v48, v37
	v_pk_add_f32 v[36:37], v[44:45], v[34:35] neg_lo:[0,1] neg_hi:[0,1]
	v_pk_add_f32 v[68:69], v[32:33], v[48:49]
	v_pk_add_f32 v[44:45], v[32:33], v[48:49] neg_lo:[0,1] neg_hi:[0,1]
	v_pk_add_f32 v[32:33], v[40:41], v[42:43]
	v_pk_add_f32 v[34:35], v[40:41], v[42:43] neg_lo:[0,1] neg_hi:[0,1]
	v_pk_add_f32 v[40:41], v[26:27], v[38:39]
	v_pk_add_f32 v[26:27], v[26:27], v[38:39] neg_lo:[0,1] neg_hi:[0,1]
	v_pk_add_f32 v[42:43], v[32:33], v[40:41] neg_lo:[0,1] neg_hi:[0,1]
	v_xor_b32_e32 v39, 0x80000000, v26
	v_mov_b32_e32 v38, v27
	v_pk_add_f32 v[26:27], v[32:33], v[40:41]
	v_pk_add_f32 v[40:41], v[20:21], v[28:29]
	v_pk_add_f32 v[20:21], v[20:21], v[28:29] neg_lo:[0,1] neg_hi:[0,1]
	v_pk_add_f32 v[32:33], v[34:35], v[38:39]
	v_pk_mul_f32 v[28:29], v[66:67], v[20:21] op_sel:[0,1] op_sel_hi:[0,0] neg_lo:[1,1] neg_hi:[1,0]
	v_pk_fma_f32 v[20:21], v[66:67], v[20:21], v[28:29] op_sel_hi:[0,1,1]
	v_pk_add_f32 v[28:29], v[22:23], v[30:31]
	v_pk_add_f32 v[22:23], v[22:23], v[30:31] neg_lo:[0,1] neg_hi:[0,1]
	v_pk_add_f32 v[38:39], v[34:35], v[38:39] neg_lo:[0,1] neg_hi:[0,1]
	v_xor_b32_e32 v31, 0x80000000, v22
	v_mov_b32_e32 v30, v23
	v_pk_add_f32 v[22:23], v[24:25], v[46:47]
	v_pk_add_f32 v[24:25], v[24:25], v[46:47] neg_lo:[0,1] neg_hi:[0,1]
	v_pk_add_f32 v[34:35], v[18:19], v[72:73]
	v_pk_mul_f32 v[46:47], v[66:67], v[24:25] op_sel:[0,1] op_sel_hi:[0,0] neg_lo:[1,1] neg_hi:[1,0]
	v_pk_fma_f32 v[24:25], v[66:67], v[24:25], v[46:47] op_sel_hi:[0,1,1] neg_lo:[1,0,0] neg_hi:[1,0,0]
	v_pk_add_f32 v[46:47], v[34:35], v[28:29]
	v_pk_add_f32 v[28:29], v[34:35], v[28:29] neg_lo:[0,1] neg_hi:[0,1]
	v_pk_add_f32 v[34:35], v[40:41], v[22:23]
	v_pk_add_f32 v[22:23], v[40:41], v[22:23] neg_lo:[0,1] neg_hi:[0,1]
	v_pk_add_f32 v[18:19], v[18:19], v[72:73] neg_lo:[0,1] neg_hi:[0,1]
	v_pk_add_f32 v[66:67], v[28:29], v[22:23] op_sel:[0,1] op_sel_hi:[1,0] neg_hi:[0,1]
	v_pk_add_f32 v[48:49], v[28:29], v[22:23] op_sel:[0,1] op_sel_hi:[1,0] neg_lo:[0,1]
	v_pk_add_f32 v[28:29], v[18:19], v[30:31]
	v_pk_add_f32 v[18:19], v[18:19], v[30:31] neg_lo:[0,1] neg_hi:[0,1]
	v_pk_add_f32 v[30:31], v[20:21], v[24:25]
	v_pk_add_f32 v[20:21], v[20:21], v[24:25] neg_lo:[0,1] neg_hi:[0,1]
	v_pk_add_f32 v[22:23], v[46:47], v[34:35]
	v_xor_b32_e32 v25, 0x80000000, v20
	v_add_u32_e32 v20, 0x2000, v16
	v_mov_b32_e32 v24, v21
	v_ashrrev_i32_e32 v21, 31, v20
	v_lshl_add_u64 v[20:21], v[20:21], 3, s[48:49]
	s_waitcnt vmcnt(0)
	v_pk_add_f32 v[40:41], v[46:47], v[34:35] neg_lo:[0,1] neg_hi:[0,1]
	v_pk_add_f32 v[34:35], v[18:19], v[24:25]
	v_pk_add_f32 v[18:19], v[18:19], v[24:25] neg_lo:[0,1] neg_hi:[0,1]
	v_pk_add_f32 v[70:71], v[28:29], v[30:31]
	v_pk_add_f32 v[46:47], v[28:29], v[30:31] neg_lo:[0,1] neg_hi:[0,1]
	s_nop 0
	v_pk_mul_f32 v[24:25], v[64:65], v[196:197] op_sel:[1,1] op_sel_hi:[1,0] neg_lo:[1,0]
	v_pk_fma_f32 v[20:21], v[64:65], v[196:197], v[24:25] op_sel_hi:[0,1,1]
	v_add_u32_e32 v24, 0x2200, v16
	v_ashrrev_i32_e32 v25, 31, v24
	v_lshl_add_u64 v[24:25], v[24:25], 3, s[48:49]
	s_nop 0
	v_pk_mul_f32 v[28:29], v[198:199], v[22:23] op_sel:[1,1] op_sel_hi:[0,1] neg_lo:[0,1]
	v_pk_fma_f32 v[22:23], v[198:199], v[22:23], v[28:29] op_sel_hi:[1,0,1]
	v_add_u32_e32 v24, 0x2400, v16
	v_ashrrev_i32_e32 v25, 31, v24
	v_lshl_add_u64 v[24:25], v[24:25], 3, s[48:49]
	s_nop 0
	v_pk_mul_f32 v[28:29], v[26:27], v[200:201] op_sel:[1,1] op_sel_hi:[1,0] neg_lo:[1,0]
	v_pk_fma_f32 v[24:25], v[26:27], v[200:201], v[28:29] op_sel_hi:[0,1,1]
	v_add_u32_e32 v26, 0x2600, v16
	v_ashrrev_i32_e32 v27, 31, v26
	v_lshl_add_u64 v[26:27], v[26:27], 3, s[48:49]
	s_nop 0
	v_pk_mul_f32 v[28:29], v[202:203], v[70:71] op_sel:[1,1] op_sel_hi:[0,1] neg_lo:[0,1]
	v_pk_fma_f32 v[26:27], v[202:203], v[70:71], v[28:29] op_sel_hi:[1,0,1]
	v_add_u32_e32 v28, 0x2800, v16
	v_ashrrev_i32_e32 v29, 31, v28
	v_lshl_add_u64 v[28:29], v[28:29], 3, s[48:49]
	s_nop 0
	v_pk_mul_f32 v[30:31], v[68:69], v[204:205] op_sel:[1,1] op_sel_hi:[1,0] neg_lo:[1,0]
	v_pk_fma_f32 v[28:29], v[68:69], v[204:205], v[30:31] op_sel_hi:[0,1,1]
	v_add_u32_e32 v30, 0x2a00, v16
	v_ashrrev_i32_e32 v31, 31, v30
	v_lshl_add_u64 v[30:31], v[30:31], 3, s[48:49]
	s_nop 0
	v_pk_mul_f32 v[64:65], v[206:207], v[66:67] op_sel:[1,1] op_sel_hi:[0,1] neg_lo:[0,1]
	v_pk_fma_f32 v[30:31], v[206:207], v[66:67], v[64:65] op_sel_hi:[1,0,1]
	v_add_u32_e32 v64, 0x2c00, v16
	v_ashrrev_i32_e32 v65, 31, v64
	v_lshl_add_u64 v[64:65], v[64:65], 3, s[48:49]
	s_nop 0
	v_pk_mul_f32 v[66:67], v[32:33], v[208:209] op_sel:[1,1] op_sel_hi:[1,0] neg_lo:[1,0]
	v_pk_fma_f32 v[32:33], v[32:33], v[208:209], v[66:67] op_sel_hi:[0,1,1]
	v_add_u32_e32 v64, 0x2e00, v16
	v_ashrrev_i32_e32 v65, 31, v64
	v_lshl_add_u64 v[64:65], v[64:65], 3, s[48:49]
	s_nop 0
	v_pk_mul_f32 v[66:67], v[210:211], v[34:35] op_sel:[1,1] op_sel_hi:[0,1] neg_lo:[0,1]
	v_pk_fma_f32 v[34:35], v[210:211], v[34:35], v[66:67] op_sel_hi:[1,0,1]
	v_add_u32_e32 v64, 0x3000, v16
	v_ashrrev_i32_e32 v65, 31, v64
	v_lshl_add_u64 v[64:65], v[64:65], 3, s[48:49]
	s_nop 0
	v_pk_mul_f32 v[66:67], v[36:37], v[212:213] op_sel:[1,1] op_sel_hi:[1,0] neg_lo:[1,0]
	v_pk_fma_f32 v[36:37], v[36:37], v[212:213], v[66:67] op_sel_hi:[0,1,1]
	v_add_u32_e32 v64, 0x3200, v16
	v_ashrrev_i32_e32 v65, 31, v64
	v_lshl_add_u64 v[64:65], v[64:65], 3, s[48:49]
	v_pk_add_f32 v[68:69], v[20:21], v[36:37]
	v_pk_add_f32 v[20:21], v[20:21], v[36:37] neg_lo:[0,1] neg_hi:[0,1]
	s_nop 0
	v_pk_mul_f32 v[66:67], v[40:41], v[214:215] op_sel:[1,1] op_sel_hi:[1,0] neg_lo:[1,0]
	v_pk_fma_f32 v[40:41], v[40:41], v[214:215], v[66:67] op_sel_hi:[0,1,1]
	v_add_u32_e32 v64, 0x3400, v16
	v_ashrrev_i32_e32 v65, 31, v64
	v_lshl_add_u64 v[64:65], v[64:65], 3, s[48:49]
	v_pk_add_f32 v[36:37], v[22:23], v[40:41]
	v_pk_add_f32 v[22:23], v[22:23], v[40:41] neg_lo:[0,1] neg_hi:[0,1]
	s_nop 0
	v_pk_mul_f32 v[66:67], v[42:43], v[216:217] op_sel:[1,1] op_sel_hi:[1,0] neg_lo:[1,0]
	v_pk_fma_f32 v[42:43], v[42:43], v[216:217], v[66:67] op_sel_hi:[0,1,1]
	v_add_u32_e32 v64, 0x3600, v16
	v_ashrrev_i32_e32 v65, 31, v64
	v_lshl_add_u64 v[64:65], v[64:65], 3, s[48:49]
	s_nop 0
	v_pk_mul_f32 v[66:67], v[46:47], v[218:219] op_sel:[1,1] op_sel_hi:[1,0] neg_lo:[1,0]
	v_pk_fma_f32 v[46:47], v[46:47], v[218:219], v[66:67] op_sel_hi:[0,1,1]
	v_add_u32_e32 v64, 0x3800, v16
	v_ashrrev_i32_e32 v65, 31, v64
	v_lshl_add_u64 v[64:65], v[64:65], 3, s[48:49]
	s_nop 0
	v_pk_mul_f32 v[66:67], v[44:45], v[220:221] op_sel:[1,1] op_sel_hi:[1,0] neg_lo:[1,0]
	v_pk_fma_f32 v[44:45], v[44:45], v[220:221], v[66:67] op_sel_hi:[0,1,1]
	v_add_u32_e32 v64, 0x3a00, v16
	v_ashrrev_i32_e32 v65, 31, v64
	v_lshl_add_u64 v[64:65], v[64:65], 3, s[48:49]
	s_nop 0
	v_pk_mul_f32 v[66:67], v[48:49], v[222:223] op_sel:[1,1] op_sel_hi:[1,0] neg_lo:[1,0]
	v_pk_fma_f32 v[48:49], v[48:49], v[222:223], v[66:67] op_sel_hi:[0,1,1]
	v_add_u32_e32 v64, 0x3c00, v16
	v_ashrrev_i32_e32 v65, 31, v64
	v_lshl_add_u64 v[64:65], v[64:65], 3, s[48:49]
	v_add_u32_e32 v16, 0x3e00, v16
	v_ashrrev_i32_e32 v17, 31, v16
	v_lshl_add_u64 v[16:17], v[16:17], 3, s[48:49]
	s_nop 0
	v_pk_mul_f32 v[66:67], v[38:39], v[224:225] op_sel:[1,1] op_sel_hi:[1,0] neg_lo:[1,0]
	v_pk_fma_f32 v[38:39], v[38:39], v[224:225], v[66:67] op_sel_hi:[0,1,1]
	s_nop 0
	v_pk_mul_f32 v[64:65], v[18:19], v[226:227] op_sel:[1,1] op_sel_hi:[1,0] neg_lo:[1,0]
	v_mov_b32_e32 v66, v170
	v_pk_fma_f32 v[16:17], v[18:19], v[226:227], v[64:65] op_sel_hi:[0,1,1]
	v_mov_b32_e32 v18, v164
	v_mov_b32_e32 v19, v167
	v_mov_b32_e32 v18, v165
	v_mov_b32_e32 v64, v168
	v_mov_b32_e32 v18, v166
	s_nop 0
	v_mov_b32_e32 v19, v169
	s_nop 0
	v_mov_b32_e32 v19, v171
	v_pk_mul_f32 v[40:41], v[22:23], v[66:67] op_sel:[1,0] op_sel_hi:[0,0] neg_lo:[1,0]
	v_mov_b32_e32 v19, v172
	s_nop 0
	v_pk_fma_f32 v[22:23], v[22:23], v[18:19], v[40:41] op_sel_hi:[1,0,1]
	v_pk_add_f32 v[40:41], v[24:25], v[42:43]
	v_pk_add_f32 v[24:25], v[24:25], v[42:43] neg_lo:[0,1] neg_hi:[0,1]
	v_pk_mul_f32 v[42:43], v[24:25], v[64:65] op_sel:[1,0] op_sel_hi:[0,0] neg_lo:[1,0]
	v_pk_fma_f32 v[24:25], v[24:25], v[64:65], v[42:43] op_sel_hi:[1,0,1]
	v_pk_add_f32 v[42:43], v[26:27], v[46:47]
	v_pk_add_f32 v[26:27], v[26:27], v[46:47] neg_lo:[0,1] neg_hi:[0,1]
	v_pk_mul_f32 v[46:47], v[26:27], v[66:67] op_sel_hi:[1,0]
	v_pk_fma_f32 v[26:27], v[26:27], v[18:19], v[46:47] op_sel:[1,0,0] op_sel_hi:[0,0,1] neg_lo:[1,0,0]
	v_pk_add_f32 v[46:47], v[28:29], v[44:45]
	v_pk_add_f32 v[28:29], v[28:29], v[44:45] neg_lo:[0,1] neg_hi:[0,1]
	v_xor_b32_e32 v44, 0x80000000, v29
	v_mov_b32_e32 v45, v28
	v_pk_add_f32 v[28:29], v[30:31], v[48:49]
	v_pk_add_f32 v[30:31], v[30:31], v[48:49] neg_lo:[0,1] neg_hi:[0,1]
	v_pk_mul_f32 v[48:49], v[30:31], v[66:67] op_sel_hi:[1,0] neg_lo:[0,1] neg_hi:[0,1]
	v_pk_fma_f32 v[30:31], v[30:31], v[18:19], v[48:49] op_sel:[1,0,0] op_sel_hi:[0,0,1] neg_lo:[1,0,0]
	v_pk_add_f32 v[48:49], v[32:33], v[38:39]
	v_pk_add_f32 v[32:33], v[32:33], v[38:39] neg_lo:[0,1] neg_hi:[0,1]
	v_pk_mul_f32 v[38:39], v[32:33], v[64:65] op_sel:[1,0] op_sel_hi:[0,0] neg_lo:[1,0]
	v_pk_fma_f32 v[32:33], v[32:33], v[64:65], v[38:39] op_sel_hi:[1,0,1] neg_lo:[0,1,0] neg_hi:[0,1,0]
	v_pk_add_f32 v[38:39], v[34:35], v[16:17]
	v_pk_add_f32 v[16:17], v[34:35], v[16:17] neg_lo:[0,1] neg_hi:[0,1]
	v_pk_mul_f32 v[34:35], v[16:17], v[66:67] op_sel:[1,0] op_sel_hi:[0,0] neg_lo:[1,0]
	v_pk_fma_f32 v[16:17], v[16:17], v[18:19], v[34:35] op_sel_hi:[1,0,1] neg_lo:[0,1,0] neg_hi:[0,1,0]
	v_pk_add_f32 v[18:19], v[68:69], v[46:47]
	v_pk_add_f32 v[34:35], v[68:69], v[46:47] neg_lo:[0,1] neg_hi:[0,1]
	v_pk_add_f32 v[46:47], v[36:37], v[28:29]
	v_pk_add_f32 v[28:29], v[36:37], v[28:29] neg_lo:[0,1] neg_hi:[0,1]
	v_pk_mul_f32 v[36:37], v[28:29], v[64:65] op_sel:[1,0] op_sel_hi:[0,0] neg_lo:[1,0]
	v_pk_fma_f32 v[28:29], v[28:29], v[64:65], v[36:37] op_sel_hi:[1,0,1]
	v_pk_add_f32 v[36:37], v[40:41], v[48:49]
	v_pk_add_f32 v[40:41], v[40:41], v[48:49] neg_lo:[0,1] neg_hi:[0,1]
	v_xor_b32_e32 v48, 0x80000000, v41
	v_mov_b32_e32 v49, v40
	v_pk_add_f32 v[40:41], v[42:43], v[38:39]
	v_pk_add_f32 v[38:39], v[42:43], v[38:39] neg_lo:[0,1] neg_hi:[0,1]
	v_pk_mul_f32 v[42:43], v[64:65], v[38:39] op_sel:[0,1] op_sel_hi:[0,0] neg_lo:[0,1]
	v_pk_fma_f32 v[38:39], v[38:39], v[64:65], v[42:43] op_sel_hi:[1,0,1] neg_lo:[0,1,0] neg_hi:[0,1,0]
	v_pk_add_f32 v[42:43], v[18:19], v[36:37]
	v_pk_add_f32 v[18:19], v[18:19], v[36:37] neg_lo:[0,1] neg_hi:[0,1]
	v_pk_add_f32 v[36:37], v[46:47], v[40:41]
	v_pk_add_f32 v[40:41], v[46:47], v[40:41] neg_lo:[0,1] neg_hi:[0,1]
	v_xor_b32_e32 v46, 0x80000000, v41
	v_mov_b32_e32 v47, v40
	v_pk_add_f32 v[40:41], v[42:43], v[36:37]
	v_pk_add_f32 v[36:37], v[42:43], v[36:37] neg_lo:[0,1] neg_hi:[0,1]
	v_pk_add_f32 v[42:43], v[18:19], v[46:47]
	v_pk_add_f32 v[18:19], v[18:19], v[46:47] neg_lo:[0,1] neg_hi:[0,1]
	v_pk_add_f32 v[46:47], v[34:35], v[48:49]
	v_pk_add_f32 v[34:35], v[34:35], v[48:49] neg_lo:[0,1] neg_hi:[0,1]
	v_pk_add_f32 v[48:49], v[28:29], v[38:39]
	v_pk_add_f32 v[28:29], v[28:29], v[38:39] neg_lo:[0,1] neg_hi:[0,1]
	v_xor_b32_e32 v38, 0x80000000, v29
	v_mov_b32_e32 v39, v28
	v_pk_add_f32 v[28:29], v[46:47], v[48:49]
	v_pk_add_f32 v[46:47], v[46:47], v[48:49] neg_lo:[0,1] neg_hi:[0,1]
	v_pk_add_f32 v[48:49], v[34:35], v[38:39]
	v_pk_add_f32 v[34:35], v[34:35], v[38:39] neg_lo:[0,1] neg_hi:[0,1]
	v_pk_add_f32 v[38:39], v[20:21], v[44:45]
	v_pk_add_f32 v[20:21], v[20:21], v[44:45] neg_lo:[0,1] neg_hi:[0,1]
	v_pk_add_f32 v[44:45], v[22:23], v[30:31]
	v_pk_add_f32 v[22:23], v[22:23], v[30:31] neg_lo:[0,1] neg_hi:[0,1]
	v_pk_mul_f32 v[30:31], v[64:65], v[22:23] op_sel:[0,1] op_sel_hi:[0,0] neg_lo:[0,1]
	v_pk_fma_f32 v[22:23], v[64:65], v[22:23], v[30:31] op_sel_hi:[0,1,1]
	v_pk_add_f32 v[30:31], v[24:25], v[32:33]
	v_pk_add_f32 v[24:25], v[24:25], v[32:33] neg_lo:[0,1] neg_hi:[0,1]
	v_xor_b32_e32 v32, 0x80000000, v25
	v_mov_b32_e32 v33, v24
	v_pk_add_f32 v[24:25], v[26:27], v[16:17]
	v_pk_add_f32 v[16:17], v[26:27], v[16:17] neg_lo:[0,1] neg_hi:[0,1]
	v_pk_mul_f32 v[26:27], v[64:65], v[16:17] op_sel:[0,1] op_sel_hi:[0,0] neg_lo:[0,1]
	v_pk_fma_f32 v[16:17], v[64:65], v[16:17], v[26:27] op_sel_hi:[0,1,1] neg_lo:[1,0,0] neg_hi:[1,0,0]
	v_pk_add_f32 v[26:27], v[38:39], v[30:31]
	v_pk_add_f32 v[30:31], v[38:39], v[30:31] neg_lo:[0,1] neg_hi:[0,1]
	v_pk_add_f32 v[38:39], v[44:45], v[24:25]
	v_pk_add_f32 v[24:25], v[44:45], v[24:25] neg_lo:[0,1] neg_hi:[0,1]
	v_xor_b32_e32 v44, 0x80000000, v25
	v_mov_b32_e32 v45, v24
	v_pk_add_f32 v[24:25], v[26:27], v[38:39]
	v_pk_add_f32 v[26:27], v[26:27], v[38:39] neg_lo:[0,1] neg_hi:[0,1]
	v_pk_add_f32 v[38:39], v[30:31], v[44:45]
	v_pk_add_f32 v[30:31], v[30:31], v[44:45] neg_lo:[0,1] neg_hi:[0,1]
	v_pk_add_f32 v[44:45], v[20:21], v[32:33]
	v_pk_add_f32 v[20:21], v[20:21], v[32:33] neg_lo:[0,1] neg_hi:[0,1]
	v_pk_add_f32 v[32:33], v[22:23], v[16:17]
	v_pk_add_f32 v[16:17], v[22:23], v[16:17] neg_lo:[0,1] neg_hi:[0,1]
	v_xor_b32_e32 v22, 0x80000000, v17
	v_mov_b32_e32 v23, v16
	v_pk_add_f32 v[16:17], v[44:45], v[32:33]
	v_pk_add_f32 v[32:33], v[44:45], v[32:33] neg_lo:[0,1] neg_hi:[0,1]
	v_pk_add_f32 v[44:45], v[20:21], v[22:23]
	v_pk_add_f32 v[20:21], v[20:21], v[22:23] neg_lo:[0,1] neg_hi:[0,1]
	ds_write_b64 v10, v[40:41]
	ds_write_b64 v13, v[24:25]
	ds_write_b64 v15, v[28:29]
	ds_write_b64 v50, v[16:17]
	ds_write_b64 v51, v[42:43]
	ds_write_b64 v52, v[38:39]
	ds_write_b64 v53, v[48:49]
	ds_write_b64 v54, v[44:45]
	ds_write_b64 v55, v[36:37]
	ds_write_b64 v56, v[26:27]
	ds_write_b64 v57, v[46:47]
	ds_write_b64 v58, v[32:33]
	ds_write_b64 v59, v[18:19]
	ds_write_b64 v60, v[30:31]
	ds_write_b64 v61, v[34:35]
	ds_write_b64 v62, v[20:21]
	v_mov_b32_e32 v10, v176
	v_mov_b32_e32 v50, v173
	s_waitcnt lgkmcnt(0)
	s_barrier
	v_add_u32_e32 v13, v50, v10
	v_lshl_add_u32 v13, v13, 3, 0
	ds_read2_b64 v[16:19], v13 offset1:16
	v_xad_u32 v15, v50, 1, v10
	v_lshl_add_u32 v15, v15, 3, 0
	s_waitcnt lgkmcnt(0)
	v_pk_fma_f32 v[16:17], v[16:17], 0, v[16:17] op_sel:[1,0,0] op_sel_hi:[0,0,1] neg_hi:[1,0,0]
	v_pk_fma_f32 v[22:23], v[182:183], s[92:93], v[182:183] op_sel:[1,0,0] op_sel_hi:[0,1,1]
	v_pk_mul_f32 v[24:25], v[22:23], v[18:19] op_sel:[1,1] op_sel_hi:[1,0] neg_hi:[0,1]
	v_pk_fma_f32 v[18:19], v[18:19], v[22:23], v[24:25] op_sel_hi:[1,0,1]
	v_pk_mul_f32 v[24:25], v[182:183], v[22:23] op_sel:[1,1] op_sel_hi:[0,1] neg_lo:[0,1]
	v_pk_fma_f32 v[26:27], v[182:183], v[22:23], v[24:25] op_sel_hi:[1,0,1]
	ds_read2_b64 v[22:25], v15 offset0:32 offset1:48
	s_waitcnt lgkmcnt(0)
	v_pk_mul_f32 v[28:29], v[22:23], v[26:27] op_sel:[1,1] op_sel_hi:[0,1] neg_hi:[1,0]
	v_pk_fma_f32 v[22:23], v[22:23], v[26:27], v[28:29] op_sel_hi:[1,0,1]
	v_pk_mul_f32 v[28:29], v[182:183], v[26:27] op_sel:[1,1] op_sel_hi:[0,1] neg_lo:[0,1]
	v_pk_fma_f32 v[26:27], v[182:183], v[26:27], v[28:29] op_sel_hi:[1,0,1]
	v_pk_mul_f32 v[28:29], v[24:25], v[26:27] op_sel:[1,1] op_sel_hi:[0,1] neg_hi:[1,0]
	v_pk_fma_f32 v[24:25], v[24:25], v[26:27], v[28:29] op_sel_hi:[1,0,1]
	v_pk_mul_f32 v[28:29], v[182:183], v[26:27] op_sel:[1,1] op_sel_hi:[0,1] neg_lo:[0,1]
	v_pk_fma_f32 v[26:27], v[182:183], v[26:27], v[28:29] op_sel_hi:[1,0,1]
	v_xad_u32 v28, v50, 2, v10
	v_lshl_add_u32 v51, v28, 3, 0
	ds_read2_b64 v[28:31], v51 offset0:64 offset1:80
	v_pk_mul_f32 v[32:33], v[182:183], v[26:27] op_sel:[1,1] op_sel_hi:[0,1] neg_lo:[0,1]
	s_waitcnt lgkmcnt(0)
	v_pk_mul_f32 v[34:35], v[28:29], v[26:27] op_sel:[1,1] op_sel_hi:[0,1] neg_hi:[1,0]
	v_pk_fma_f32 v[28:29], v[28:29], v[26:27], v[34:35] op_sel_hi:[1,0,1]
	v_pk_fma_f32 v[34:35], v[182:183], v[26:27], v[32:33] op_sel_hi:[1,0,1]
	v_pk_mul_f32 v[26:27], v[30:31], v[34:35] op_sel:[1,1] op_sel_hi:[0,1] neg_hi:[1,0]
	v_pk_fma_f32 v[26:27], v[30:31], v[34:35], v[26:27] op_sel_hi:[1,0,1]
	v_xad_u32 v30, v50, 3, v10
	v_lshl_add_u32 v54, v30, 3, 0
	ds_read2_b64 v[30:33], v54 offset0:96 offset1:112
	v_pk_mul_f32 v[36:37], v[182:183], v[34:35] op_sel:[1,1] op_sel_hi:[0,1] neg_lo:[0,1]
	v_pk_fma_f32 v[34:35], v[182:183], v[34:35], v[36:37] op_sel_hi:[1,0,1]
	s_waitcnt lgkmcnt(0)
	v_pk_mul_f32 v[36:37], v[30:31], v[34:35] op_sel:[1,1] op_sel_hi:[0,1] neg_hi:[1,0]
	v_pk_fma_f32 v[30:31], v[30:31], v[34:35], v[36:37] op_sel_hi:[1,0,1]
	v_pk_mul_f32 v[36:37], v[182:183], v[34:35] op_sel:[1,1] op_sel_hi:[0,1] neg_lo:[0,1]
	v_pk_fma_f32 v[34:35], v[182:183], v[34:35], v[36:37] op_sel_hi:[1,0,1]
	v_pk_mul_f32 v[36:37], v[32:33], v[34:35] op_sel:[1,1] op_sel_hi:[0,1] neg_hi:[1,0]
	v_pk_fma_f32 v[32:33], v[32:33], v[34:35], v[36:37] op_sel_hi:[1,0,1]
	v_pk_mul_f32 v[36:37], v[182:183], v[34:35] op_sel:[1,1] op_sel_hi:[0,1] neg_lo:[0,1]
	v_pk_fma_f32 v[38:39], v[182:183], v[34:35], v[36:37] op_sel_hi:[1,0,1]
	v_xad_u32 v34, v50, 4, v10
	v_lshl_add_u32 v55, v34, 3, 0
	ds_read2_b64 v[34:37], v55 offset0:128 offset1:144
	v_pk_mul_f32 v[40:41], v[182:183], v[38:39] op_sel:[1,1] op_sel_hi:[0,1] neg_lo:[0,1]
	s_waitcnt lgkmcnt(0)
	v_pk_mul_f32 v[42:43], v[34:35], v[38:39] op_sel:[1,1] op_sel_hi:[0,1] neg_hi:[1,0]
	v_pk_fma_f32 v[34:35], v[34:35], v[38:39], v[42:43] op_sel_hi:[1,0,1]
	v_pk_fma_f32 v[42:43], v[182:183], v[38:39], v[40:41] op_sel_hi:[1,0,1]
	v_pk_mul_f32 v[38:39], v[36:37], v[42:43] op_sel:[1,1] op_sel_hi:[0,1] neg_hi:[1,0]
	v_pk_fma_f32 v[36:37], v[36:37], v[42:43], v[38:39] op_sel_hi:[1,0,1]
	v_xad_u32 v38, v50, 5, v10
	v_lshl_add_u32 v56, v38, 3, 0
	ds_read2_b64 v[38:41], v56 offset0:160 offset1:176
	v_pk_mul_f32 v[44:45], v[182:183], v[42:43] op_sel:[1,1] op_sel_hi:[0,1] neg_lo:[0,1]
	v_pk_fma_f32 v[42:43], v[182:183], v[42:43], v[44:45] op_sel_hi:[1,0,1]
	s_waitcnt lgkmcnt(0)
	v_pk_mul_f32 v[44:45], v[38:39], v[42:43] op_sel:[1,1] op_sel_hi:[0,1] neg_hi:[1,0]
	v_pk_fma_f32 v[38:39], v[38:39], v[42:43], v[44:45] op_sel_hi:[1,0,1]
	v_pk_mul_f32 v[44:45], v[182:183], v[42:43] op_sel:[1,1] op_sel_hi:[0,1] neg_lo:[0,1]
	v_pk_fma_f32 v[42:43], v[182:183], v[42:43], v[44:45] op_sel_hi:[1,0,1]
	v_pk_mul_f32 v[44:45], v[40:41], v[42:43] op_sel:[1,1] op_sel_hi:[0,1] neg_hi:[1,0]
	v_pk_fma_f32 v[40:41], v[40:41], v[42:43], v[44:45] op_sel_hi:[1,0,1]
	v_pk_mul_f32 v[44:45], v[182:183], v[42:43] op_sel:[1,1] op_sel_hi:[0,1] neg_lo:[0,1]
	v_pk_fma_f32 v[42:43], v[182:183], v[42:43], v[44:45] op_sel_hi:[1,0,1]
	v_xad_u32 v44, v50, 6, v10
	v_lshl_add_u32 v57, v44, 3, 0
	ds_read2_b64 v[44:47], v57 offset0:192 offset1:208
	v_pk_mul_f32 v[48:49], v[182:183], v[42:43] op_sel:[1,1] op_sel_hi:[0,1] neg_lo:[0,1]
	s_waitcnt lgkmcnt(0)
	v_pk_mul_f32 v[52:53], v[44:45], v[42:43] op_sel:[1,1] op_sel_hi:[0,1] neg_hi:[1,0]
	v_pk_fma_f32 v[44:45], v[44:45], v[42:43], v[52:53] op_sel_hi:[1,0,1]
	v_pk_fma_f32 v[52:53], v[182:183], v[42:43], v[48:49] op_sel_hi:[1,0,1]
	v_pk_mul_f32 v[42:43], v[46:47], v[52:53] op_sel:[1,1] op_sel_hi:[0,1] neg_hi:[1,0]
	v_pk_fma_f32 v[42:43], v[46:47], v[52:53], v[42:43] op_sel_hi:[1,0,1]
	v_xad_u32 v46, v50, 7, v10
	v_lshl_add_u32 v58, v46, 3, 0
	ds_read2_b64 v[46:49], v58 offset0:224 offset1:240
	v_pk_mul_f32 v[60:61], v[182:183], v[52:53] op_sel:[1,1] op_sel_hi:[0,1] neg_lo:[0,1]
	v_pk_fma_f32 v[52:53], v[182:183], v[52:53], v[60:61] op_sel_hi:[1,0,1]
	s_waitcnt lgkmcnt(0)
	v_pk_mul_f32 v[60:61], v[46:47], v[52:53] op_sel:[1,1] op_sel_hi:[0,1] neg_hi:[1,0]
	v_pk_fma_f32 v[46:47], v[46:47], v[52:53], v[60:61] op_sel_hi:[1,0,1]
	v_pk_mul_f32 v[60:61], v[182:183], v[52:53] op_sel:[1,1] op_sel_hi:[0,1] neg_lo:[0,1]
	v_pk_fma_f32 v[52:53], v[182:183], v[52:53], v[60:61] op_sel_hi:[1,0,1]
	v_pk_mul_f32 v[60:61], v[48:49], v[52:53] op_sel:[1,1] op_sel_hi:[0,1] neg_hi:[1,0]
	v_pk_fma_f32 v[48:49], v[48:49], v[52:53], v[60:61] op_sel_hi:[1,0,1]
	v_pk_mul_f32 v[60:61], v[182:183], v[52:53] op_sel:[1,1] op_sel_hi:[0,1] neg_lo:[0,1]
	v_pk_fma_f32 v[64:65], v[182:183], v[52:53], v[60:61] op_sel_hi:[1,0,1]
	v_xad_u32 v52, v50, 8, v10
	v_lshl_add_u32 v52, v52, 3, 0
	v_add_u32_e32 v59, 0x800, v52
	ds_read2_b64 v[60:63], v59 offset1:16
	v_pk_mul_f32 v[66:67], v[182:183], v[64:65] op_sel:[1,1] op_sel_hi:[0,1] neg_lo:[0,1]
	v_pk_fma_f32 v[66:67], v[182:183], v[64:65], v[66:67] op_sel_hi:[1,0,1]
	s_waitcnt lgkmcnt(0)
	v_pk_mul_f32 v[52:53], v[60:61], v[64:65] op_sel:[1,1] op_sel_hi:[0,1] neg_hi:[1,0]
	v_pk_fma_f32 v[52:53], v[60:61], v[64:65], v[52:53] op_sel_hi:[1,0,1]
	v_pk_mul_f32 v[60:61], v[62:63], v[66:67] op_sel:[1,1] op_sel_hi:[0,1] neg_hi:[1,0]
	v_pk_fma_f32 v[70:71], v[62:63], v[66:67], v[60:61] op_sel_hi:[1,0,1]
	v_xad_u32 v60, v50, 9, v10
	v_lshl_add_u32 v60, v60, 3, 0
	v_add_u32_e32 v60, 0x800, v60
	ds_read2_b64 v[62:65], v60 offset0:32 offset1:48
	v_pk_mul_f32 v[68:69], v[182:183], v[66:67] op_sel:[1,1] op_sel_hi:[0,1] neg_lo:[0,1]
	v_pk_fma_f32 v[66:67], v[182:183], v[66:67], v[68:69] op_sel_hi:[1,0,1]
	s_waitcnt lgkmcnt(0)
	v_pk_mul_f32 v[68:69], v[62:63], v[66:67] op_sel:[1,1] op_sel_hi:[0,1] neg_hi:[1,0]
	v_pk_fma_f32 v[72:73], v[62:63], v[66:67], v[68:69] op_sel_hi:[1,0,1]
	v_pk_mul_f32 v[62:63], v[182:183], v[66:67] op_sel:[1,1] op_sel_hi:[0,1] neg_lo:[0,1]
	v_pk_fma_f32 v[62:63], v[182:183], v[66:67], v[62:63] op_sel_hi:[1,0,1]
	v_pk_mul_f32 v[66:67], v[64:65], v[62:63] op_sel:[1,1] op_sel_hi:[0,1] neg_hi:[1,0]
	v_pk_fma_f32 v[74:75], v[64:65], v[62:63], v[66:67] op_sel_hi:[1,0,1]
	v_pk_mul_f32 v[64:65], v[182:183], v[62:63] op_sel:[1,1] op_sel_hi:[0,1] neg_lo:[0,1]
	v_pk_fma_f32 v[66:67], v[182:183], v[62:63], v[64:65] op_sel_hi:[1,0,1]
	v_xad_u32 v61, v50, 10, v10
	v_lshl_add_u32 v61, v61, 3, 0
	v_add_u32_e32 v61, 0x800, v61
	ds_read2_b64 v[62:65], v61 offset0:64 offset1:80
	v_pk_mul_f32 v[68:69], v[182:183], v[66:67] op_sel:[1,1] op_sel_hi:[0,1] neg_lo:[0,1]
	v_pk_fma_f32 v[68:69], v[182:183], v[66:67], v[68:69] op_sel_hi:[1,0,1]
	s_waitcnt lgkmcnt(0)
	v_pk_mul_f32 v[76:77], v[62:63], v[66:67] op_sel:[1,1] op_sel_hi:[0,1] neg_hi:[1,0]
	v_pk_fma_f32 v[76:77], v[62:63], v[66:67], v[76:77] op_sel_hi:[1,0,1]
	v_pk_mul_f32 v[62:63], v[64:65], v[68:69] op_sel:[1,1] op_sel_hi:[0,1] neg_hi:[1,0]
	v_pk_fma_f32 v[78:79], v[64:65], v[68:69], v[62:63] op_sel_hi:[1,0,1]
	v_xad_u32 v62, v50, 11, v10
	v_lshl_add_u32 v62, v62, 3, 0
	v_add_u32_e32 v62, 0x800, v62
	ds_read2_b64 v[64:67], v62 offset0:96 offset1:112
	v_pk_mul_f32 v[80:81], v[182:183], v[68:69] op_sel:[1,1] op_sel_hi:[0,1] neg_lo:[0,1]
	v_pk_fma_f32 v[68:69], v[182:183], v[68:69], v[80:81] op_sel_hi:[1,0,1]
	s_waitcnt lgkmcnt(0)
	v_pk_mul_f32 v[80:81], v[64:65], v[68:69] op_sel:[1,1] op_sel_hi:[0,1] neg_hi:[1,0]
	v_pk_fma_f32 v[80:81], v[64:65], v[68:69], v[80:81] op_sel_hi:[1,0,1]
	v_pk_mul_f32 v[64:65], v[182:183], v[68:69] op_sel:[1,1] op_sel_hi:[0,1] neg_lo:[0,1]
	v_pk_fma_f32 v[64:65], v[182:183], v[68:69], v[64:65] op_sel_hi:[1,0,1]
	v_pk_mul_f32 v[68:69], v[66:67], v[64:65] op_sel:[1,1] op_sel_hi:[0,1] neg_hi:[1,0]
	v_pk_fma_f32 v[82:83], v[66:67], v[64:65], v[68:69] op_sel_hi:[1,0,1]
	v_pk_mul_f32 v[66:67], v[182:183], v[64:65] op_sel:[1,1] op_sel_hi:[0,1] neg_lo:[0,1]
	v_pk_fma_f32 v[68:69], v[182:183], v[64:65], v[66:67] op_sel_hi:[1,0,1]
	v_xad_u32 v63, v50, 12, v10
	v_lshl_add_u32 v63, v63, 3, 0
	v_add_u32_e32 v63, 0x800, v63
	ds_read2_b64 v[64:67], v63 offset0:128 offset1:144
	v_pk_mul_f32 v[84:85], v[182:183], v[68:69] op_sel:[1,1] op_sel_hi:[0,1] neg_lo:[0,1]
	v_pk_fma_f32 v[84:85], v[182:183], v[68:69], v[84:85] op_sel_hi:[1,0,1]
	s_waitcnt lgkmcnt(0)
	v_pk_mul_f32 v[86:87], v[64:65], v[68:69] op_sel:[1,1] op_sel_hi:[0,1] neg_hi:[1,0]
	v_pk_fma_f32 v[86:87], v[64:65], v[68:69], v[86:87] op_sel_hi:[1,0,1]
	v_pk_mul_f32 v[64:65], v[66:67], v[84:85] op_sel:[1,1] op_sel_hi:[0,1] neg_hi:[1,0]
	v_pk_fma_f32 v[88:89], v[66:67], v[84:85], v[64:65] op_sel_hi:[1,0,1]
	v_xad_u32 v64, v50, 13, v10
	v_lshl_add_u32 v64, v64, 3, 0
	v_add_u32_e32 v64, 0x800, v64
	ds_read2_b64 v[66:69], v64 offset0:160 offset1:176
	v_pk_mul_f32 v[90:91], v[182:183], v[84:85] op_sel:[1,1] op_sel_hi:[0,1] neg_lo:[0,1]
	v_pk_fma_f32 v[84:85], v[182:183], v[84:85], v[90:91] op_sel_hi:[1,0,1]
	s_waitcnt lgkmcnt(0)
	v_pk_mul_f32 v[90:91], v[66:67], v[84:85] op_sel:[1,1] op_sel_hi:[0,1] neg_hi:[1,0]
	v_pk_fma_f32 v[90:91], v[66:67], v[84:85], v[90:91] op_sel_hi:[1,0,1]
	v_pk_mul_f32 v[66:67], v[182:183], v[84:85] op_sel:[1,1] op_sel_hi:[0,1] neg_lo:[0,1]
	v_pk_fma_f32 v[66:67], v[182:183], v[84:85], v[66:67] op_sel_hi:[1,0,1]
	v_pk_mul_f32 v[84:85], v[68:69], v[66:67] op_sel:[1,1] op_sel_hi:[0,1] neg_hi:[1,0]
	v_pk_fma_f32 v[84:85], v[68:69], v[66:67], v[84:85] op_sel_hi:[1,0,1]
	v_pk_mul_f32 v[68:69], v[182:183], v[66:67] op_sel:[1,1] op_sel_hi:[0,1] neg_lo:[0,1]
	v_pk_fma_f32 v[92:93], v[182:183], v[66:67], v[68:69] op_sel_hi:[1,0,1]
	v_xad_u32 v65, v50, 14, v10
	v_lshl_add_u32 v65, v65, 3, 0
	v_add_u32_e32 v65, 0x800, v65
	ds_read2_b64 v[66:69], v65 offset0:192 offset1:208
	v_pk_mul_f32 v[94:95], v[182:183], v[92:93] op_sel:[1,1] op_sel_hi:[0,1] neg_lo:[0,1]
	v_xad_u32 v10, v50, 15, v10
	s_waitcnt lgkmcnt(0)
	v_pk_mul_f32 v[96:97], v[66:67], v[92:93] op_sel:[1,1] op_sel_hi:[0,1] neg_hi:[1,0]
	v_lshl_add_u32 v10, v10, 3, 0
	v_pk_fma_f32 v[96:97], v[66:67], v[92:93], v[96:97] op_sel_hi:[1,0,1]
	v_pk_fma_f32 v[92:93], v[182:183], v[92:93], v[94:95] op_sel_hi:[1,0,1]
	v_pk_mul_f32 v[66:67], v[68:69], v[92:93] op_sel:[1,1] op_sel_hi:[0,1] neg_hi:[1,0]
	v_add_u32_e32 v101, 0x800, v10
	v_pk_fma_f32 v[94:95], v[68:69], v[92:93], v[66:67] op_sel_hi:[1,0,1]
	ds_read2_b64 v[66:69], v101 offset0:224 offset1:240
	v_pk_mul_f32 v[98:99], v[182:183], v[92:93] op_sel:[1,1] op_sel_hi:[0,1] neg_lo:[0,1]
	v_pk_fma_f32 v[92:93], v[182:183], v[92:93], v[98:99] op_sel_hi:[1,0,1]
	s_waitcnt lgkmcnt(0)
	v_pk_mul_f32 v[98:99], v[66:67], v[92:93] op_sel:[1,1] op_sel_hi:[0,1] neg_hi:[1,0]
	v_pk_fma_f32 v[66:67], v[66:67], v[92:93], v[98:99] op_sel_hi:[1,0,1]
	v_pk_mul_f32 v[98:99], v[182:183], v[92:93] op_sel:[1,1] op_sel_hi:[0,1] neg_lo:[0,1]
	v_pk_fma_f32 v[20:21], v[182:183], v[92:93], v[98:99] op_sel_hi:[1,0,1]
	v_pk_mul_f32 v[92:93], v[68:69], v[20:21] op_sel:[1,1] op_sel_hi:[0,1] neg_hi:[1,0]
	v_pk_fma_f32 v[68:69], v[68:69], v[20:21], v[92:93] op_sel_hi:[1,0,1]
	v_mov_b32_e32 v10, v164
	v_pk_add_f32 v[104:105], v[16:17], v[52:53]
	v_pk_add_f32 v[16:17], v[16:17], v[52:53] neg_lo:[0,1] neg_hi:[0,1]
	v_pk_add_f32 v[52:53], v[18:19], v[70:71]
	v_pk_add_f32 v[18:19], v[18:19], v[70:71] neg_lo:[0,1] neg_hi:[0,1]
	v_mov_b32_e32 v92, v165
	v_mov_b32_e32 v20, v166
	v_mov_b32_e32 v98, v167
	v_mov_b32_e32 v10, v168
	v_mov_b32_e32 v100, v169
	v_mov_b32_e32 v50, v170
	v_mov_b32_e32 v102, v171
	v_mov_b32_e32 v21, v172
	v_pk_mul_f32 v[70:71], v[102:103], v[18:19] op_sel:[0,1] op_sel_hi:[0,0] neg_lo:[0,1]
	v_pk_fma_f32 v[18:19], v[92:93], v[18:19], v[70:71] op_sel_hi:[0,1,1]
	v_pk_add_f32 v[70:71], v[22:23], v[72:73]
	v_pk_add_f32 v[22:23], v[22:23], v[72:73] neg_lo:[0,1] neg_hi:[0,1]
	v_pk_mul_f32 v[72:73], v[50:51], v[22:23] op_sel:[0,1] op_sel_hi:[0,0] neg_lo:[0,1]
	v_pk_fma_f32 v[22:23], v[20:21], v[22:23], v[72:73] op_sel_hi:[0,1,1]
	v_pk_add_f32 v[72:73], v[24:25], v[74:75]
	v_pk_add_f32 v[24:25], v[24:25], v[74:75] neg_lo:[0,1] neg_hi:[0,1]
	v_pk_mul_f32 v[74:75], v[100:101], v[24:25] op_sel:[0,1] op_sel_hi:[0,0] neg_lo:[0,1]
	v_pk_fma_f32 v[24:25], v[98:99], v[24:25], v[74:75] op_sel_hi:[0,1,1]
	v_pk_add_f32 v[74:75], v[28:29], v[76:77]
	v_pk_add_f32 v[28:29], v[28:29], v[76:77] neg_lo:[0,1] neg_hi:[0,1]
	v_pk_mul_f32 v[76:77], v[10:11], v[28:29] op_sel:[0,1] op_sel_hi:[0,0] neg_lo:[0,1]
	v_pk_fma_f32 v[28:29], v[10:11], v[28:29], v[76:77] op_sel_hi:[0,1,1]
	v_pk_add_f32 v[76:77], v[26:27], v[78:79]
	v_pk_add_f32 v[26:27], v[26:27], v[78:79] neg_lo:[0,1] neg_hi:[0,1]
	v_pk_mul_f32 v[78:79], v[98:99], v[26:27] op_sel:[0,1] op_sel_hi:[0,0] neg_lo:[0,1]
	v_pk_fma_f32 v[26:27], v[100:101], v[26:27], v[78:79] op_sel_hi:[0,1,1]
	v_pk_add_f32 v[78:79], v[30:31], v[80:81]
	v_pk_add_f32 v[30:31], v[30:31], v[80:81] neg_lo:[0,1] neg_hi:[0,1]
	v_pk_mul_f32 v[80:81], v[20:21], v[30:31] op_sel:[0,1] op_sel_hi:[0,0] neg_lo:[0,1]
	v_pk_fma_f32 v[30:31], v[50:51], v[30:31], v[80:81] op_sel_hi:[0,1,1]
	v_pk_add_f32 v[80:81], v[32:33], v[82:83]
	v_pk_add_f32 v[32:33], v[32:33], v[82:83] neg_lo:[0,1] neg_hi:[0,1]
	v_pk_mul_f32 v[82:83], v[92:93], v[32:33] op_sel:[0,1] op_sel_hi:[0,0] neg_lo:[0,1]
	v_pk_fma_f32 v[32:33], v[102:103], v[32:33], v[82:83] op_sel_hi:[0,1,1]
	v_pk_add_f32 v[82:83], v[34:35], v[86:87]
	v_pk_add_f32 v[34:35], v[34:35], v[86:87] neg_lo:[0,1] neg_hi:[0,1]
	v_xor_b32_e32 v86, 0x80000000, v35
	v_mov_b32_e32 v87, v34
	v_pk_add_f32 v[34:35], v[36:37], v[88:89]
	v_pk_add_f32 v[36:37], v[36:37], v[88:89] neg_lo:[0,1] neg_hi:[0,1]
	v_pk_mul_f32 v[88:89], v[92:93], v[36:37] op_sel:[0,1] op_sel_hi:[0,0] neg_lo:[0,1]
	v_pk_fma_f32 v[36:37], v[102:103], v[36:37], v[88:89] op_sel_hi:[0,1,1] neg_lo:[1,0,0] neg_hi:[1,0,0]
	v_pk_add_f32 v[88:89], v[38:39], v[90:91]
	v_pk_add_f32 v[38:39], v[38:39], v[90:91] neg_lo:[0,1] neg_hi:[0,1]
	v_pk_mul_f32 v[90:91], v[20:21], v[38:39] op_sel:[0,1] op_sel_hi:[0,0] neg_lo:[0,1]
	v_pk_fma_f32 v[38:39], v[50:51], v[38:39], v[90:91] op_sel_hi:[0,1,1] neg_lo:[1,0,0] neg_hi:[1,0,0]
	v_pk_add_f32 v[90:91], v[40:41], v[84:85]
	v_pk_add_f32 v[40:41], v[40:41], v[84:85] neg_lo:[0,1] neg_hi:[0,1]
	v_pk_mul_f32 v[84:85], v[98:99], v[40:41] op_sel:[0,1] op_sel_hi:[0,0] neg_lo:[0,1]
	v_pk_fma_f32 v[40:41], v[100:101], v[40:41], v[84:85] op_sel_hi:[0,1,1] neg_lo:[1,0,0] neg_hi:[1,0,0]
	v_pk_add_f32 v[84:85], v[44:45], v[96:97]
	v_pk_add_f32 v[44:45], v[44:45], v[96:97] neg_lo:[0,1] neg_hi:[0,1]
	v_pk_mul_f32 v[96:97], v[10:11], v[44:45] op_sel:[0,1] op_sel_hi:[0,0] neg_lo:[0,1]
	v_pk_fma_f32 v[44:45], v[10:11], v[44:45], v[96:97] op_sel_hi:[0,1,1] neg_lo:[1,0,0] neg_hi:[1,0,0]
	v_pk_add_f32 v[96:97], v[42:43], v[94:95]
	v_pk_add_f32 v[42:43], v[42:43], v[94:95] neg_lo:[0,1] neg_hi:[0,1]
	v_pk_mul_f32 v[94:95], v[100:101], v[42:43] op_sel:[0,1] op_sel_hi:[0,0] neg_lo:[0,1]
	v_pk_fma_f32 v[42:43], v[98:99], v[42:43], v[94:95] op_sel_hi:[0,1,1] neg_lo:[1,0,0] neg_hi:[1,0,0]
	v_pk_add_f32 v[94:95], v[46:47], v[66:67]
	v_pk_add_f32 v[46:47], v[46:47], v[66:67] neg_lo:[0,1] neg_hi:[0,1]
	v_pk_mul_f32 v[66:67], v[50:51], v[46:47] op_sel:[0,1] op_sel_hi:[0,0] neg_lo:[0,1]
	v_pk_fma_f32 v[46:47], v[20:21], v[46:47], v[66:67] op_sel_hi:[0,1,1] neg_lo:[1,0,0] neg_hi:[1,0,0]
	v_pk_add_f32 v[66:67], v[48:49], v[68:69]
	v_pk_add_f32 v[48:49], v[48:49], v[68:69] neg_lo:[0,1] neg_hi:[0,1]
	v_pk_mul_f32 v[68:69], v[102:103], v[48:49] op_sel:[0,1] op_sel_hi:[0,0] neg_lo:[0,1]
	v_pk_fma_f32 v[48:49], v[92:93], v[48:49], v[68:69] op_sel_hi:[0,1,1] neg_lo:[1,0,0] neg_hi:[1,0,0]
	v_pk_add_f32 v[92:93], v[52:53], v[34:35]
	v_pk_add_f32 v[34:35], v[52:53], v[34:35] neg_lo:[0,1] neg_hi:[0,1]
	v_pk_add_f32 v[68:69], v[104:105], v[82:83]
	v_pk_mul_f32 v[52:53], v[50:51], v[34:35] op_sel:[0,1] op_sel_hi:[0,0] neg_lo:[0,1]
	v_pk_fma_f32 v[34:35], v[20:21], v[34:35], v[52:53] op_sel_hi:[0,1,1]
	v_pk_add_f32 v[52:53], v[70:71], v[88:89]
	v_pk_add_f32 v[70:71], v[70:71], v[88:89] neg_lo:[0,1] neg_hi:[0,1]
	v_pk_add_f32 v[82:83], v[104:105], v[82:83] neg_lo:[0,1] neg_hi:[0,1]
	v_pk_mul_f32 v[88:89], v[10:11], v[70:71] op_sel:[0,1] op_sel_hi:[0,0] neg_lo:[0,1]
	v_pk_fma_f32 v[70:71], v[10:11], v[70:71], v[88:89] op_sel_hi:[0,1,1]
	v_pk_add_f32 v[88:89], v[72:73], v[90:91]
	v_pk_add_f32 v[72:73], v[72:73], v[90:91] neg_lo:[0,1] neg_hi:[0,1]
	v_pk_mul_f32 v[90:91], v[20:21], v[72:73] op_sel:[0,1] op_sel_hi:[0,0] neg_lo:[0,1]
	v_pk_fma_f32 v[72:73], v[50:51], v[72:73], v[90:91] op_sel_hi:[0,1,1]
	v_pk_add_f32 v[90:91], v[74:75], v[84:85]
	v_pk_add_f32 v[74:75], v[74:75], v[84:85] neg_lo:[0,1] neg_hi:[0,1]
	v_xor_b32_e32 v84, 0x80000000, v75
	v_mov_b32_e32 v85, v74
	v_pk_add_f32 v[74:75], v[76:77], v[96:97]
	v_pk_add_f32 v[76:77], v[76:77], v[96:97] neg_lo:[0,1] neg_hi:[0,1]
	v_pk_mul_f32 v[96:97], v[20:21], v[76:77] op_sel:[0,1] op_sel_hi:[0,0] neg_lo:[0,1]
	v_pk_fma_f32 v[76:77], v[50:51], v[76:77], v[96:97] op_sel_hi:[0,1,1] neg_lo:[1,0,0] neg_hi:[1,0,0]
	v_pk_add_f32 v[96:97], v[78:79], v[94:95]
	v_pk_add_f32 v[78:79], v[78:79], v[94:95] neg_lo:[0,1] neg_hi:[0,1]
	v_pk_mul_f32 v[94:95], v[10:11], v[78:79] op_sel:[0,1] op_sel_hi:[0,0] neg_lo:[0,1]
	v_pk_fma_f32 v[78:79], v[10:11], v[78:79], v[94:95] op_sel_hi:[0,1,1] neg_lo:[1,0,0] neg_hi:[1,0,0]
	v_pk_add_f32 v[94:95], v[80:81], v[66:67]
	v_pk_add_f32 v[66:67], v[80:81], v[66:67] neg_lo:[0,1] neg_hi:[0,1]
	v_pk_mul_f32 v[80:81], v[50:51], v[66:67] op_sel:[0,1] op_sel_hi:[0,0] neg_lo:[0,1]
	v_pk_fma_f32 v[66:67], v[20:21], v[66:67], v[80:81] op_sel_hi:[0,1,1] neg_lo:[1,0,0] neg_hi:[1,0,0]
	v_pk_add_f32 v[80:81], v[68:69], v[90:91]
	v_pk_add_f32 v[68:69], v[68:69], v[90:91] neg_lo:[0,1] neg_hi:[0,1]
	v_pk_add_f32 v[90:91], v[92:93], v[74:75]
	v_pk_add_f32 v[74:75], v[92:93], v[74:75] neg_lo:[0,1] neg_hi:[0,1]
	v_pk_mul_f32 v[92:93], v[10:11], v[74:75] op_sel:[0,1] op_sel_hi:[0,0] neg_lo:[0,1]
	v_pk_fma_f32 v[74:75], v[10:11], v[74:75], v[92:93] op_sel_hi:[0,1,1]
	v_pk_add_f32 v[92:93], v[52:53], v[96:97]
	v_pk_add_f32 v[52:53], v[52:53], v[96:97] neg_lo:[0,1] neg_hi:[0,1]
	v_xor_b32_e32 v96, 0x80000000, v53
	v_mov_b32_e32 v97, v52
	v_pk_add_f32 v[52:53], v[88:89], v[94:95]
	v_pk_add_f32 v[88:89], v[88:89], v[94:95] neg_lo:[0,1] neg_hi:[0,1]
	v_pk_mul_f32 v[94:95], v[10:11], v[88:89] op_sel:[0,1] op_sel_hi:[0,0] neg_lo:[0,1]
	v_pk_fma_f32 v[88:89], v[10:11], v[88:89], v[94:95] op_sel_hi:[0,1,1] neg_lo:[1,0,0] neg_hi:[1,0,0]
	v_pk_add_f32 v[94:95], v[80:81], v[92:93]
	v_pk_add_f32 v[80:81], v[80:81], v[92:93] neg_lo:[0,1] neg_hi:[0,1]
	v_pk_add_f32 v[92:93], v[90:91], v[52:53]
	v_pk_add_f32 v[52:53], v[90:91], v[52:53] neg_lo:[0,1] neg_hi:[0,1]
	v_xor_b32_e32 v90, 0x80000000, v53
	v_mov_b32_e32 v91, v52
	v_pk_add_f32 v[52:53], v[94:95], v[92:93]
	v_pk_add_f32 v[92:93], v[94:95], v[92:93] neg_lo:[0,1] neg_hi:[0,1]
	v_pk_add_f32 v[94:95], v[80:81], v[90:91]
	v_pk_add_f32 v[80:81], v[80:81], v[90:91] neg_lo:[0,1] neg_hi:[0,1]
	v_pk_add_f32 v[90:91], v[68:69], v[96:97]
	v_pk_add_f32 v[68:69], v[68:69], v[96:97] neg_lo:[0,1] neg_hi:[0,1]
	v_pk_add_f32 v[96:97], v[74:75], v[88:89]
	v_pk_add_f32 v[74:75], v[74:75], v[88:89] neg_lo:[0,1] neg_hi:[0,1]
	v_xor_b32_e32 v88, 0x80000000, v75
	v_mov_b32_e32 v89, v74
	v_pk_add_f32 v[74:75], v[90:91], v[96:97]
	v_pk_add_f32 v[90:91], v[90:91], v[96:97] neg_lo:[0,1] neg_hi:[0,1]
	v_pk_add_f32 v[96:97], v[68:69], v[88:89]
	v_pk_add_f32 v[68:69], v[68:69], v[88:89] neg_lo:[0,1] neg_hi:[0,1]
	v_pk_add_f32 v[88:89], v[82:83], v[84:85]
	v_pk_add_f32 v[82:83], v[82:83], v[84:85] neg_lo:[0,1] neg_hi:[0,1]
	v_pk_add_f32 v[84:85], v[34:35], v[76:77]
	v_pk_add_f32 v[34:35], v[34:35], v[76:77] neg_lo:[0,1] neg_hi:[0,1]
	v_pk_mul_f32 v[76:77], v[10:11], v[34:35] op_sel:[0,1] op_sel_hi:[0,0] neg_lo:[0,1]
	v_pk_fma_f32 v[34:35], v[10:11], v[34:35], v[76:77] op_sel_hi:[0,1,1]
	v_pk_add_f32 v[76:77], v[70:71], v[78:79]
	v_pk_add_f32 v[70:71], v[70:71], v[78:79] neg_lo:[0,1] neg_hi:[0,1]
	v_xor_b32_e32 v78, 0x80000000, v71
	v_mov_b32_e32 v79, v70
	v_pk_add_f32 v[70:71], v[72:73], v[66:67]
	v_pk_add_f32 v[66:67], v[72:73], v[66:67] neg_lo:[0,1] neg_hi:[0,1]
	v_pk_mul_f32 v[72:73], v[10:11], v[66:67] op_sel:[0,1] op_sel_hi:[0,0] neg_lo:[0,1]
	v_pk_fma_f32 v[66:67], v[10:11], v[66:67], v[72:73] op_sel_hi:[0,1,1] neg_lo:[1,0,0] neg_hi:[1,0,0]
	v_pk_add_f32 v[72:73], v[88:89], v[76:77]
	v_pk_add_f32 v[76:77], v[88:89], v[76:77] neg_lo:[0,1] neg_hi:[0,1]
	v_pk_add_f32 v[88:89], v[84:85], v[70:71]
	v_pk_add_f32 v[70:71], v[84:85], v[70:71] neg_lo:[0,1] neg_hi:[0,1]
	v_xor_b32_e32 v84, 0x80000000, v71
	v_mov_b32_e32 v85, v70
	v_pk_add_f32 v[70:71], v[72:73], v[88:89]
	v_pk_add_f32 v[72:73], v[72:73], v[88:89] neg_lo:[0,1] neg_hi:[0,1]
	v_pk_add_f32 v[88:89], v[76:77], v[84:85]
	v_pk_add_f32 v[76:77], v[76:77], v[84:85] neg_lo:[0,1] neg_hi:[0,1]
	v_pk_add_f32 v[84:85], v[82:83], v[78:79]
	v_pk_add_f32 v[78:79], v[82:83], v[78:79] neg_lo:[0,1] neg_hi:[0,1]
	v_pk_add_f32 v[82:83], v[34:35], v[66:67]
	v_pk_add_f32 v[34:35], v[34:35], v[66:67] neg_lo:[0,1] neg_hi:[0,1]
	v_xor_b32_e32 v66, 0x80000000, v35
	v_mov_b32_e32 v67, v34
	v_pk_add_f32 v[34:35], v[84:85], v[82:83]
	v_pk_add_f32 v[82:83], v[84:85], v[82:83] neg_lo:[0,1] neg_hi:[0,1]
	v_pk_add_f32 v[84:85], v[78:79], v[66:67]
	v_pk_add_f32 v[66:67], v[78:79], v[66:67] neg_lo:[0,1] neg_hi:[0,1]
	v_pk_add_f32 v[78:79], v[16:17], v[86:87]
	v_pk_add_f32 v[16:17], v[16:17], v[86:87] neg_lo:[0,1] neg_hi:[0,1]
	v_pk_add_f32 v[86:87], v[18:19], v[36:37]
	v_pk_add_f32 v[18:19], v[18:19], v[36:37] neg_lo:[0,1] neg_hi:[0,1]
	v_pk_mul_f32 v[36:37], v[50:51], v[18:19] op_sel:[0,1] op_sel_hi:[0,0] neg_lo:[0,1]
	v_pk_fma_f32 v[18:19], v[20:21], v[18:19], v[36:37] op_sel_hi:[0,1,1]
	v_pk_add_f32 v[36:37], v[22:23], v[38:39]
	v_pk_add_f32 v[22:23], v[22:23], v[38:39] neg_lo:[0,1] neg_hi:[0,1]
	v_pk_mul_f32 v[38:39], v[10:11], v[22:23] op_sel:[0,1] op_sel_hi:[0,0] neg_lo:[0,1]
	v_pk_fma_f32 v[22:23], v[10:11], v[22:23], v[38:39] op_sel_hi:[0,1,1]
	v_pk_add_f32 v[38:39], v[24:25], v[40:41]
	v_pk_add_f32 v[24:25], v[24:25], v[40:41] neg_lo:[0,1] neg_hi:[0,1]
	v_pk_mul_f32 v[40:41], v[20:21], v[24:25] op_sel:[0,1] op_sel_hi:[0,0] neg_lo:[0,1]
	v_pk_fma_f32 v[24:25], v[50:51], v[24:25], v[40:41] op_sel_hi:[0,1,1]
	v_pk_add_f32 v[40:41], v[28:29], v[44:45]
	v_pk_add_f32 v[28:29], v[28:29], v[44:45] neg_lo:[0,1] neg_hi:[0,1]
	v_xor_b32_e32 v44, 0x80000000, v29
	v_mov_b32_e32 v45, v28
	v_pk_add_f32 v[28:29], v[26:27], v[42:43]
	v_pk_add_f32 v[26:27], v[26:27], v[42:43] neg_lo:[0,1] neg_hi:[0,1]
	v_pk_mul_f32 v[42:43], v[20:21], v[26:27] op_sel:[0,1] op_sel_hi:[0,0] neg_lo:[0,1]
	v_pk_fma_f32 v[26:27], v[50:51], v[26:27], v[42:43] op_sel_hi:[0,1,1] neg_lo:[1,0,0] neg_hi:[1,0,0]
	v_pk_add_f32 v[42:43], v[30:31], v[46:47]
	v_pk_add_f32 v[30:31], v[30:31], v[46:47] neg_lo:[0,1] neg_hi:[0,1]
	v_pk_mul_f32 v[46:47], v[10:11], v[30:31] op_sel:[0,1] op_sel_hi:[0,0] neg_lo:[0,1]
	v_pk_fma_f32 v[30:31], v[10:11], v[30:31], v[46:47] op_sel_hi:[0,1,1] neg_lo:[1,0,0] neg_hi:[1,0,0]
	v_pk_add_f32 v[46:47], v[32:33], v[48:49]
	v_pk_add_f32 v[32:33], v[32:33], v[48:49] neg_lo:[0,1] neg_hi:[0,1]
	v_pk_mul_f32 v[48:49], v[50:51], v[32:33] op_sel:[0,1] op_sel_hi:[0,0] neg_lo:[0,1]
	v_pk_fma_f32 v[20:21], v[20:21], v[32:33], v[48:49] op_sel_hi:[0,1,1] neg_lo:[1,0,0] neg_hi:[1,0,0]
	v_pk_add_f32 v[48:49], v[86:87], v[28:29]
	v_pk_add_f32 v[28:29], v[86:87], v[28:29] neg_lo:[0,1] neg_hi:[0,1]
	v_pk_add_f32 v[32:33], v[78:79], v[40:41]
	v_pk_add_f32 v[40:41], v[78:79], v[40:41] neg_lo:[0,1] neg_hi:[0,1]
	v_pk_mul_f32 v[78:79], v[10:11], v[28:29] op_sel:[0,1] op_sel_hi:[0,0] neg_lo:[0,1]
	v_pk_fma_f32 v[28:29], v[10:11], v[28:29], v[78:79] op_sel_hi:[0,1,1]
	v_pk_add_f32 v[78:79], v[36:37], v[42:43]
	v_pk_add_f32 v[36:37], v[36:37], v[42:43] neg_lo:[0,1] neg_hi:[0,1]
	v_xor_b32_e32 v42, 0x80000000, v37
	v_mov_b32_e32 v43, v36
	v_pk_add_f32 v[36:37], v[38:39], v[46:47]
	v_pk_add_f32 v[38:39], v[38:39], v[46:47] neg_lo:[0,1] neg_hi:[0,1]
	v_pk_mul_f32 v[46:47], v[10:11], v[38:39] op_sel:[0,1] op_sel_hi:[0,0] neg_lo:[0,1]
	v_pk_fma_f32 v[38:39], v[10:11], v[38:39], v[46:47] op_sel_hi:[0,1,1] neg_lo:[1,0,0] neg_hi:[1,0,0]
	v_pk_add_f32 v[46:47], v[32:33], v[78:79]
	v_pk_add_f32 v[32:33], v[32:33], v[78:79] neg_lo:[0,1] neg_hi:[0,1]
	v_pk_add_f32 v[78:79], v[48:49], v[36:37]
	v_pk_add_f32 v[36:37], v[48:49], v[36:37] neg_lo:[0,1] neg_hi:[0,1]
	v_pk_add_f32 v[86:87], v[32:33], v[36:37] op_sel:[0,1] op_sel_hi:[1,0] neg_lo:[0,1]
	v_pk_add_f32 v[32:33], v[32:33], v[36:37] op_sel:[0,1] op_sel_hi:[1,0] neg_hi:[0,1]
	v_pk_add_f32 v[48:49], v[40:41], v[42:43]
	v_pk_add_f32 v[40:41], v[40:41], v[42:43] neg_lo:[0,1] neg_hi:[0,1]
	v_pk_add_f32 v[42:43], v[28:29], v[38:39]
	v_pk_add_f32 v[28:29], v[28:29], v[38:39] neg_lo:[0,1] neg_hi:[0,1]
	v_pk_add_f32 v[36:37], v[46:47], v[78:79] neg_lo:[0,1] neg_hi:[0,1]
	v_xor_b32_e32 v38, 0x80000000, v29
	v_mov_b32_e32 v39, v28
	v_pk_add_f32 v[28:29], v[48:49], v[42:43]
	v_pk_add_f32 v[42:43], v[48:49], v[42:43] neg_lo:[0,1] neg_hi:[0,1]
	v_pk_add_f32 v[48:49], v[40:41], v[38:39]
	v_pk_add_f32 v[38:39], v[40:41], v[38:39] neg_lo:[0,1] neg_hi:[0,1]
	v_pk_add_f32 v[40:41], v[16:17], v[44:45]
	v_pk_add_f32 v[16:17], v[16:17], v[44:45] neg_lo:[0,1] neg_hi:[0,1]
	v_pk_add_f32 v[44:45], v[18:19], v[26:27]
	v_pk_add_f32 v[18:19], v[18:19], v[26:27] neg_lo:[0,1] neg_hi:[0,1]
	v_pk_mul_f32 v[26:27], v[10:11], v[18:19] op_sel:[0,1] op_sel_hi:[0,0] neg_lo:[0,1]
	v_pk_fma_f32 v[18:19], v[10:11], v[18:19], v[26:27] op_sel_hi:[0,1,1]
	v_pk_add_f32 v[26:27], v[22:23], v[30:31]
	v_pk_add_f32 v[22:23], v[22:23], v[30:31] neg_lo:[0,1] neg_hi:[0,1]
	v_xor_b32_e32 v30, 0x80000000, v23
	v_mov_b32_e32 v31, v22
	v_pk_add_f32 v[22:23], v[24:25], v[20:21]
	v_pk_add_f32 v[20:21], v[24:25], v[20:21] neg_lo:[0,1] neg_hi:[0,1]
	v_pk_mul_f32 v[24:25], v[10:11], v[20:21] op_sel:[0,1] op_sel_hi:[0,0] neg_lo:[0,1]
	v_pk_fma_f32 v[20:21], v[10:11], v[20:21], v[24:25] op_sel_hi:[0,1,1] neg_lo:[1,0,0] neg_hi:[1,0,0]
	v_pk_add_f32 v[24:25], v[40:41], v[26:27]
	v_pk_add_f32 v[26:27], v[40:41], v[26:27] neg_lo:[0,1] neg_hi:[0,1]
	v_pk_add_f32 v[40:41], v[44:45], v[22:23]
	v_pk_add_f32 v[22:23], v[44:45], v[22:23] neg_lo:[0,1] neg_hi:[0,1]
	v_xor_b32_e32 v44, 0x80000000, v23
	v_mov_b32_e32 v45, v22
	v_pk_add_f32 v[22:23], v[24:25], v[40:41]
	v_pk_add_f32 v[24:25], v[24:25], v[40:41] neg_lo:[0,1] neg_hi:[0,1]
	v_pk_add_f32 v[40:41], v[26:27], v[44:45]
	v_pk_add_f32 v[26:27], v[26:27], v[44:45] neg_lo:[0,1] neg_hi:[0,1]
	v_pk_add_f32 v[44:45], v[16:17], v[30:31]
	v_pk_add_f32 v[16:17], v[16:17], v[30:31] neg_lo:[0,1] neg_hi:[0,1]
	v_pk_add_f32 v[30:31], v[18:19], v[20:21]
	v_pk_add_f32 v[18:19], v[18:19], v[20:21] neg_lo:[0,1] neg_hi:[0,1]
	v_xor_b32_e32 v20, 0x80000000, v19
	v_mov_b32_e32 v21, v18
	v_pk_add_f32 v[18:19], v[44:45], v[30:31]
	v_pk_add_f32 v[30:31], v[44:45], v[30:31] neg_lo:[0,1] neg_hi:[0,1]
	v_pk_add_f32 v[44:45], v[16:17], v[20:21]
	v_pk_add_f32 v[16:17], v[16:17], v[20:21] neg_lo:[0,1] neg_hi:[0,1]
	v_pk_add_f32 v[20:21], v[46:47], v[78:79]
	ds_write2_b64 v13, v[52:53], v[20:21] offset1:16
	ds_write2_b64 v15, v[70:71], v[22:23] offset0:32 offset1:48
	ds_write2_b64 v51, v[74:75], v[28:29] offset0:64 offset1:80
	ds_write2_b64 v54, v[34:35], v[18:19] offset0:96 offset1:112
	ds_write2_b64 v55, v[94:95], v[86:87] offset0:128 offset1:144
	ds_write2_b64 v56, v[88:89], v[40:41] offset0:160 offset1:176
	ds_write2_b64 v57, v[96:97], v[48:49] offset0:192 offset1:208
	ds_write2_b64 v58, v[84:85], v[44:45] offset0:224 offset1:240
	ds_write2_b64 v59, v[92:93], v[36:37] offset1:16
	ds_write2_b64 v60, v[72:73], v[24:25] offset0:32 offset1:48
	ds_write2_b64 v61, v[90:91], v[42:43] offset0:64 offset1:80
	ds_write2_b64 v62, v[82:83], v[30:31] offset0:96 offset1:112
	ds_write2_b64 v63, v[80:81], v[32:33] offset0:128 offset1:144
	ds_write2_b64 v64, v[76:77], v[26:27] offset0:160 offset1:176
	ds_write2_b64 v65, v[68:69], v[38:39] offset0:192 offset1:208
	ds_write2_b64 v101, v[66:67], v[16:17] offset0:224 offset1:240
	v_mov_b32_e32 v10, v174
	s_waitcnt lgkmcnt(0)
	s_barrier
	v_lshl_add_u32 v10, v10, 3, 0
	ds_read_b64 v[16:17], v10
	ds_read_b64 v[80:81], v10 offset:4224
	ds_read_b64 v[78:79], v10 offset:8448
	ds_read_b64 v[76:77], v10 offset:12672
	ds_read_b64 v[74:75], v10 offset:16896
	ds_read_b64 v[72:73], v10 offset:21120
	ds_read_b64 v[70:71], v10 offset:25344
	ds_read_b64 v[68:69], v10 offset:29568
	ds_read_b64 v[24:25], v10 offset:33792
	ds_read_b64 v[62:63], v10 offset:38016
	ds_read_b64 v[60:61], v10 offset:42240
	ds_read_b64 v[58:59], v10 offset:46464
	ds_read_b64 v[54:55], v10 offset:50688
	ds_read_b64 v[50:51], v10 offset:54912
	ds_read_b64 v[46:47], v10 offset:59136
	ds_read_b64 v[44:45], v10 offset:63360
	v_add_u32_e32 v13, 0x10800, v10
	v_add_u32_e32 v15, 0x11880, v10
	v_add_u32_e32 v20, 0x12900, v10
	v_add_u32_e32 v21, 0x13980, v10
	ds_read_b64 v[18:19], v13
	ds_read_b64 v[66:67], v15
	ds_read_b64 v[64:65], v20
	ds_read_b64 v[38:39], v21
	v_add_u32_e32 v13, 0x14a00, v10
	v_add_u32_e32 v15, 0x15a80, v10
	v_add_u32_e32 v20, 0x16b00, v10
	v_add_u32_e32 v21, 0x17b80, v10
	ds_read_b64 v[30:31], v13
	ds_read_b64 v[56:57], v15
	ds_read_b64 v[52:53], v20
	ds_read_b64 v[48:49], v21
	v_add_u32_e32 v13, 0x18c00, v10
	v_add_u32_e32 v15, 0x19c80, v10
	v_add_u32_e32 v20, 0x1ad00, v10
	v_add_u32_e32 v21, 0x1bd80, v10
	ds_read_b64 v[82:83], v13
	ds_read_b64 v[42:43], v15
	ds_read_b64 v[40:41], v20
	ds_read_b64 v[36:37], v21
	v_add_u32_e32 v13, 0x1ce00, v10
	v_add_u32_e32 v15, 0x1de80, v10
	v_add_u32_e32 v20, 0x1ef00, v10
	v_add_u32_e32 v10, 0x1ff80, v10
	ds_read_b64 v[34:35], v13
	ds_read_b64 v[32:33], v15
	ds_read_b64 v[28:29], v20
	ds_read_b64 v[26:27], v10
	v_pk_fma_f32 v[84:85], v[180:181], s[92:93], v[180:181] op_sel:[1,0,0] op_sel_hi:[0,1,1]
	v_pk_mul_f32 v[20:21], v[180:181], v[84:85] op_sel:[1,1] op_sel_hi:[0,1] neg_lo:[0,1]
	v_pk_fma_f32 v[86:87], v[180:181], v[84:85], v[20:21] op_sel_hi:[1,0,1]
	v_mov_b32_e32 v10, v164
	v_pk_mul_f32 v[20:21], v[180:181], v[86:87] op_sel:[1,1] op_sel_hi:[0,1] neg_lo:[0,1]
	v_pk_fma_f32 v[88:89], v[180:181], v[86:87], v[20:21] op_sel_hi:[1,0,1]
	s_waitcnt lgkmcnt(14)
	v_fmac_f32_e32 v16, 0, v17
	v_pk_mul_f32 v[20:21], v[180:181], v[88:89] op_sel:[1,1] op_sel_hi:[0,1] neg_lo:[0,1]
	v_pk_fma_f32 v[90:91], v[180:181], v[88:89], v[20:21] op_sel_hi:[1,0,1]
	v_mov_b32_e32 v10, v165
	v_pk_mul_f32 v[20:21], v[180:181], v[90:91] op_sel:[1,1] op_sel_hi:[0,1] neg_lo:[0,1]
	v_pk_fma_f32 v[92:93], v[180:181], v[90:91], v[20:21] op_sel_hi:[1,0,1]
	v_mov_b32_e32 v13, v172
	v_pk_mul_f32 v[20:21], v[180:181], v[92:93] op_sel:[1,1] op_sel_hi:[0,1] neg_lo:[0,1]
	v_pk_fma_f32 v[94:95], v[180:181], v[92:93], v[20:21] op_sel_hi:[1,0,1]
	v_readlane_b32 s72, v251, 48
	v_pk_mul_f32 v[20:21], v[180:181], v[94:95] op_sel:[1,1] op_sel_hi:[0,1] neg_lo:[0,1]
	v_pk_fma_f32 v[96:97], v[180:181], v[94:95], v[20:21] op_sel_hi:[1,0,1]
	v_readlane_b32 s73, v251, 49
	v_pk_mul_f32 v[20:21], v[180:181], v[96:97] op_sel:[1,1] op_sel_hi:[0,1] neg_lo:[0,1]
	v_pk_fma_f32 v[98:99], v[180:181], v[96:97], v[20:21] op_sel_hi:[1,0,1]
	s_movk_i32 s10, 0xda00
	v_pk_mul_f32 v[20:21], v[180:181], v[98:99] op_sel:[1,1] op_sel_hi:[0,1] neg_lo:[0,1]
	v_pk_fma_f32 v[100:101], v[180:181], v[98:99], v[20:21] op_sel_hi:[1,0,1]
	s_mov_b32 s20, 0x3f61c598
	v_pk_mul_f32 v[20:21], v[180:181], v[100:101] op_sel:[1,1] op_sel_hi:[0,1] neg_lo:[0,1]
	v_pk_fma_f32 v[102:103], v[180:181], v[100:101], v[20:21] op_sel_hi:[1,0,1]
	s_mov_b32 s52, s95
	v_pk_mul_f32 v[20:21], v[180:181], v[102:103] op_sel:[1,1] op_sel_hi:[0,1] neg_lo:[0,1]
	v_pk_fma_f32 v[104:105], v[180:181], v[102:103], v[20:21] op_sel_hi:[1,0,1]
	s_mov_b32 s53, s94
	v_pk_mul_f32 v[20:21], v[180:181], v[104:105] op_sel:[1,1] op_sel_hi:[0,1] neg_lo:[0,1]
	v_pk_fma_f32 v[106:107], v[180:181], v[104:105], v[20:21] op_sel_hi:[1,0,1]
	s_mov_b32 s21, 0xbef15aea
	v_pk_mul_f32 v[20:21], v[180:181], v[106:107] op_sel:[1,1] op_sel_hi:[0,1] neg_lo:[0,1]
	v_pk_fma_f32 v[108:109], v[180:181], v[106:107], v[20:21] op_sel_hi:[1,0,1]
	s_mov_b32 s40, s47
	v_pk_mul_f32 v[20:21], v[180:181], v[108:109] op_sel:[1,1] op_sel_hi:[0,1] neg_lo:[0,1]
	v_pk_fma_f32 v[110:111], v[180:181], v[108:109], v[20:21] op_sel_hi:[1,0,1]
	s_mov_b32 s41, s42
	v_pk_mul_f32 v[20:21], v[180:181], v[110:111] op_sel:[1,1] op_sel_hi:[0,1] neg_lo:[0,1]
	v_pk_fma_f32 v[112:113], v[180:181], v[110:111], v[20:21] op_sel_hi:[1,0,1]
	s_mov_b32 s38, 0x3f3504f3
	v_pk_mul_f32 v[20:21], v[180:181], v[112:113] op_sel:[1,1] op_sel_hi:[0,1] neg_lo:[0,1]
	v_pk_fma_f32 v[20:21], v[180:181], v[112:113], v[20:21] op_sel_hi:[1,0,1]
	s_mov_b32 s39, 0xbf3504f3
	v_pk_mul_f32 v[114:115], v[180:181], v[20:21] op_sel:[1,1] op_sel_hi:[0,1] neg_lo:[0,1]
	v_pk_fma_f32 v[114:115], v[180:181], v[20:21], v[114:115] op_sel_hi:[1,0,1]
	v_mul_f32_e32 v18, v18, v20
	v_pk_mul_f32 v[116:117], v[180:181], v[114:115] op_sel:[1,1] op_sel_hi:[0,1] neg_lo:[0,1]
	v_pk_fma_f32 v[116:117], v[180:181], v[114:115], v[116:117] op_sel_hi:[1,0,1]
	v_fmac_f32_e32 v18, v19, v21
	v_pk_mul_f32 v[118:119], v[180:181], v[116:117] op_sel:[1,1] op_sel_hi:[0,1] neg_lo:[0,1]
	v_pk_fma_f32 v[118:119], v[180:181], v[116:117], v[118:119] op_sel_hi:[1,0,1]
	v_add_f32_e32 v17, v16, v18
	v_pk_mul_f32 v[120:121], v[180:181], v[118:119] op_sel:[1,1] op_sel_hi:[0,1] neg_lo:[0,1]
	v_pk_fma_f32 v[120:121], v[180:181], v[118:119], v[120:121] op_sel_hi:[1,0,1]
	s_mov_b32 s28, 0x3f226799
	v_pk_mul_f32 v[122:123], v[180:181], v[120:121] op_sel:[1,1] op_sel_hi:[0,1] neg_lo:[0,1]
	v_pk_fma_f32 v[122:123], v[180:181], v[120:121], v[122:123] op_sel_hi:[1,0,1]
	s_mov_b32 s29, 0xbf45e403
	v_pk_mul_f32 v[124:125], v[180:181], v[122:123] op_sel:[1,1] op_sel_hi:[0,1] neg_lo:[0,1]
	v_pk_fma_f32 v[124:125], v[180:181], v[122:123], v[124:125] op_sel_hi:[1,0,1]
	s_mov_b32 s82, 0x3f0e39da
	v_pk_mul_f32 v[126:127], v[180:181], v[124:125] op_sel:[1,1] op_sel_hi:[0,1] neg_lo:[0,1]
	v_pk_fma_f32 v[126:127], v[180:181], v[124:125], v[126:127] op_sel_hi:[1,0,1]
	s_mov_b32 s83, 0xbf54db31
	v_pk_mul_f32 v[128:129], v[180:181], v[126:127] op_sel:[1,1] op_sel_hi:[0,1] neg_lo:[0,1]
	v_pk_fma_f32 v[128:129], v[180:181], v[126:127], v[128:129] op_sel_hi:[1,0,1]
	s_mov_b32 s22, 0x3ef15aea
	v_pk_mul_f32 v[130:131], v[180:181], v[128:129] op_sel:[1,1] op_sel_hi:[0,1] neg_lo:[0,1]
	v_pk_fma_f32 v[130:131], v[180:181], v[128:129], v[130:131] op_sel_hi:[1,0,1]
	s_mov_b32 s23, 0xbf61c598
	v_pk_mul_f32 v[132:133], v[180:181], v[130:131] op_sel:[1,1] op_sel_hi:[0,1] neg_lo:[0,1]
	v_pk_fma_f32 v[132:133], v[180:181], v[130:131], v[132:133] op_sel_hi:[1,0,1]
	s_mov_b32 s18, 0x3ec3ef15
	v_pk_mul_f32 v[134:135], v[180:181], v[132:133] op_sel:[1,1] op_sel_hi:[0,1] neg_lo:[0,1]
	v_pk_fma_f32 v[134:135], v[180:181], v[132:133], v[134:135] op_sel_hi:[1,0,1]
	s_mov_b32 s19, 0xbf6c835e
	v_pk_mul_f32 v[136:137], v[180:181], v[134:135] op_sel:[1,1] op_sel_hi:[0,1] neg_lo:[0,1]
	v_pk_fma_f32 v[136:137], v[180:181], v[134:135], v[136:137] op_sel_hi:[1,0,1]
	s_mov_b32 s24, 0x3f54db31
	v_pk_mul_f32 v[138:139], v[180:181], v[136:137] op_sel:[1,1] op_sel_hi:[0,1] neg_lo:[0,1]
	v_pk_fma_f32 v[138:139], v[180:181], v[136:137], v[138:139] op_sel_hi:[1,0,1]
	s_mov_b32 s25, 0xbf0e39da
	v_pk_mul_f32 v[140:141], v[180:181], v[138:139] op_sel:[1,1] op_sel_hi:[0,1] neg_lo:[0,1]
	v_pk_fma_f32 v[140:141], v[180:181], v[138:139], v[140:141] op_sel_hi:[1,0,1]
	s_mov_b32 s74, 0x3f45e403
	v_pk_mul_f32 v[142:143], v[180:181], v[140:141] op_sel:[1,1] op_sel_hi:[0,1] neg_lo:[0,1]
	v_pk_fma_f32 v[22:23], v[180:181], v[140:141], v[142:143] op_sel_hi:[1,0,1]
	s_waitcnt lgkmcnt(0)
	v_pk_mul_f32 v[142:143], v[26:27], v[22:23] op_sel:[1,1] op_sel_hi:[0,1] neg_hi:[1,0]
	s_mov_b32 s75, 0xbf226799
	v_pk_fma_f32 v[26:27], v[26:27], v[22:23], v[142:143] op_sel_hi:[1,0,1]
	v_pk_mul_f32 v[22:23], v[28:29], v[140:141] op_sel:[1,1] op_sel_hi:[0,1] neg_hi:[1,0]
	s_mov_b32 s36, s77
	v_pk_fma_f32 v[28:29], v[28:29], v[140:141], v[22:23] op_sel_hi:[1,0,1]
	v_pk_mul_f32 v[22:23], v[32:33], v[138:139] op_sel:[1,1] op_sel_hi:[0,1] neg_hi:[1,0]
	s_mov_b32 s37, s43
	v_pk_fma_f32 v[32:33], v[32:33], v[138:139], v[22:23] op_sel_hi:[1,0,1]
	v_pk_mul_f32 v[22:23], v[34:35], v[136:137] op_sel:[1,1] op_sel_hi:[0,1] neg_hi:[1,0]
	s_mov_b32 s76, s43
	v_pk_fma_f32 v[34:35], v[34:35], v[136:137], v[22:23] op_sel_hi:[1,0,1]
	v_pk_mul_f32 v[22:23], v[36:37], v[134:135] op_sel:[1,1] op_sel_hi:[0,1] neg_hi:[1,0]
	s_mov_b32 s16, 0x3f6c835e
	v_pk_fma_f32 v[36:37], v[36:37], v[134:135], v[22:23] op_sel_hi:[1,0,1]
	v_pk_mul_f32 v[22:23], v[40:41], v[132:133] op_sel:[1,1] op_sel_hi:[0,1] neg_hi:[1,0]
	s_mov_b32 s17, 0xbec3ef15
	v_pk_fma_f32 v[40:41], v[40:41], v[132:133], v[22:23] op_sel_hi:[1,0,1]
	v_pk_mul_f32 v[22:23], v[42:43], v[130:131] op_sel:[1,1] op_sel_hi:[0,1] neg_hi:[1,0]
	s_mov_b32 s16, s19
	v_pk_fma_f32 v[42:43], v[42:43], v[130:131], v[22:23] op_sel_hi:[1,0,1]
	v_pk_mul_f32 v[22:23], v[82:83], v[128:129] op_sel:[1,1] op_sel_hi:[0,1] neg_hi:[1,0]
	s_mov_b32 s27, s29
	v_pk_fma_f32 v[22:23], v[82:83], v[128:129], v[22:23] op_sel_hi:[1,0,1]
	v_pk_mul_f32 v[82:83], v[48:49], v[126:127] op_sel:[1,1] op_sel_hi:[0,1] neg_hi:[1,0]
	s_mov_b32 s26, s75
	v_pk_fma_f32 v[48:49], v[48:49], v[126:127], v[82:83] op_sel_hi:[1,0,1]
	v_pk_mul_f32 v[82:83], v[52:53], v[124:125] op_sel:[1,1] op_sel_hi:[0,1] neg_hi:[1,0]
	s_mov_b32 s46, s42
	v_pk_fma_f32 v[52:53], v[52:53], v[124:125], v[82:83] op_sel_hi:[1,0,1]
	v_pk_mul_f32 v[82:83], v[56:57], v[122:123] op_sel:[1,1] op_sel_hi:[0,1] neg_hi:[1,0]
	v_mov_b32_e32 v124, v171
	v_pk_fma_f32 v[56:57], v[56:57], v[122:123], v[82:83] op_sel_hi:[1,0,1]
	v_pk_mul_f32 v[82:83], v[30:31], v[120:121] op_sel:[1,1] op_sel_hi:[0,1] neg_hi:[1,0]
	v_mov_b32_e32 v122, v169
	v_pk_fma_f32 v[30:31], v[30:31], v[120:121], v[82:83] op_sel_hi:[1,0,1]
	v_pk_mul_f32 v[82:83], v[38:39], v[118:119] op_sel:[1,1] op_sel_hi:[0,1] neg_hi:[1,0]
	v_mov_b32_e32 v120, v167
	v_pk_fma_f32 v[38:39], v[38:39], v[118:119], v[82:83] op_sel_hi:[1,0,1]
	v_pk_mul_f32 v[82:83], v[64:65], v[116:117] op_sel:[1,1] op_sel_hi:[0,1] neg_hi:[1,0]
	v_mov_b32_e32 v118, v165
	v_pk_fma_f32 v[64:65], v[64:65], v[116:117], v[82:83] op_sel_hi:[1,0,1]
	v_pk_mul_f32 v[82:83], v[66:67], v[114:115] op_sel:[1,1] op_sel_hi:[0,1] neg_hi:[1,0]
	v_pk_fma_f32 v[66:67], v[66:67], v[114:115], v[82:83] op_sel_hi:[1,0,1]
	v_pk_mul_f32 v[82:83], v[44:45], v[112:113] op_sel:[1,1] op_sel_hi:[0,1] neg_hi:[1,0]
	v_pk_fma_f32 v[44:45], v[44:45], v[112:113], v[82:83] op_sel_hi:[1,0,1]
	v_pk_mul_f32 v[82:83], v[46:47], v[110:111] op_sel:[1,1] op_sel_hi:[0,1] neg_hi:[1,0]
	v_pk_fma_f32 v[46:47], v[46:47], v[110:111], v[82:83] op_sel_hi:[1,0,1]
	v_pk_mul_f32 v[82:83], v[50:51], v[108:109] op_sel:[1,1] op_sel_hi:[0,1] neg_hi:[1,0]
	v_pk_fma_f32 v[50:51], v[50:51], v[108:109], v[82:83] op_sel_hi:[1,0,1]
	v_pk_mul_f32 v[82:83], v[54:55], v[106:107] op_sel:[1,1] op_sel_hi:[0,1] neg_hi:[1,0]
	v_pk_fma_f32 v[54:55], v[54:55], v[106:107], v[82:83] op_sel_hi:[1,0,1]
	v_pk_mul_f32 v[82:83], v[58:59], v[104:105] op_sel:[1,1] op_sel_hi:[0,1] neg_hi:[1,0]
	v_pk_fma_f32 v[58:59], v[58:59], v[104:105], v[82:83] op_sel_hi:[1,0,1]
	v_pk_mul_f32 v[82:83], v[60:61], v[102:103] op_sel:[1,1] op_sel_hi:[0,1] neg_hi:[1,0]
	v_pk_fma_f32 v[60:61], v[60:61], v[102:103], v[82:83] op_sel_hi:[1,0,1]
	v_pk_mul_f32 v[82:83], v[62:63], v[100:101] op_sel:[1,1] op_sel_hi:[0,1] neg_hi:[1,0]
	v_pk_fma_f32 v[62:63], v[62:63], v[100:101], v[82:83] op_sel_hi:[1,0,1]
	v_pk_mul_f32 v[82:83], v[24:25], v[98:99] op_sel:[1,1] op_sel_hi:[0,1] neg_hi:[1,0]
	v_pk_fma_f32 v[24:25], v[24:25], v[98:99], v[82:83] op_sel_hi:[1,0,1]
	v_pk_mul_f32 v[82:83], v[68:69], v[96:97] op_sel:[1,1] op_sel_hi:[0,1] neg_hi:[1,0]
	v_add_f32_e32 v22, v24, v22
	v_pk_fma_f32 v[68:69], v[68:69], v[96:97], v[82:83] op_sel_hi:[1,0,1]
	v_pk_mul_f32 v[82:83], v[70:71], v[94:95] op_sel:[1,1] op_sel_hi:[0,1] neg_hi:[1,0]
	v_add_f32_e32 v20, v17, v22
	v_pk_fma_f32 v[70:71], v[70:71], v[94:95], v[82:83] op_sel_hi:[1,0,1]
	v_pk_mul_f32 v[82:83], v[72:73], v[92:93] op_sel:[1,1] op_sel_hi:[0,1] neg_hi:[1,0]
	v_mov_b32_e32 v94, v171
	v_pk_fma_f32 v[72:73], v[72:73], v[92:93], v[82:83] op_sel_hi:[1,0,1]
	v_pk_mul_f32 v[82:83], v[74:75], v[90:91] op_sel:[1,1] op_sel_hi:[0,1] neg_hi:[1,0]
	v_mov_b32_e32 v92, v170
	v_pk_fma_f32 v[74:75], v[74:75], v[90:91], v[82:83] op_sel_hi:[1,0,1]
	v_pk_mul_f32 v[82:83], v[76:77], v[88:89] op_sel:[1,1] op_sel_hi:[0,1] neg_hi:[1,0]
	v_mov_b32_e32 v90, v169
	v_pk_fma_f32 v[76:77], v[76:77], v[88:89], v[82:83] op_sel_hi:[1,0,1]
	v_pk_mul_f32 v[82:83], v[78:79], v[86:87] op_sel:[1,1] op_sel_hi:[0,1] neg_hi:[1,0]
	v_mov_b32_e32 v88, v168
	v_pk_fma_f32 v[78:79], v[78:79], v[86:87], v[82:83] op_sel_hi:[1,0,1]
	v_pk_mul_f32 v[82:83], v[84:85], v[80:81] op_sel:[1,1] op_sel_hi:[1,0] neg_hi:[0,1]
	v_mov_b32_e32 v86, v167
	v_pk_fma_f32 v[80:81], v[80:81], v[84:85], v[82:83] op_sel_hi:[1,0,1]
	v_mov_b32_e32 v84, v166
	v_pk_add_f32 v[96:97], v[80:81], v[66:67]
	v_pk_add_f32 v[66:67], v[80:81], v[66:67] neg_lo:[0,1] neg_hi:[0,1]
	s_nop 0
	v_sub_f32_e32 v82, v25, v23
	v_pk_mul_f32 v[80:81], v[94:95], v[66:67] op_sel:[0,1] op_sel_hi:[0,0] neg_lo:[0,1]
	v_pk_fma_f32 v[80:81], v[10:11], v[66:67], v[80:81] op_sel_hi:[0,1,1]
	v_pk_add_f32 v[66:67], v[78:79], v[64:65]
	v_pk_add_f32 v[64:65], v[78:79], v[64:65] neg_lo:[0,1] neg_hi:[0,1]
	v_pk_mul_f32 v[78:79], v[92:93], v[64:65] op_sel:[0,1] op_sel_hi:[0,0] neg_lo:[0,1]
	v_pk_fma_f32 v[64:65], v[84:85], v[64:65], v[78:79] op_sel_hi:[0,1,1]
	v_pk_add_f32 v[78:79], v[76:77], v[38:39]
	v_pk_add_f32 v[38:39], v[76:77], v[38:39] neg_lo:[0,1] neg_hi:[0,1]
	s_barrier
	v_pk_mul_f32 v[76:77], v[90:91], v[38:39] op_sel:[0,1] op_sel_hi:[0,0] neg_lo:[0,1]
	v_pk_fma_f32 v[76:77], v[86:87], v[38:39], v[76:77] op_sel_hi:[0,1,1]
	v_pk_add_f32 v[38:39], v[74:75], v[30:31]
	v_pk_add_f32 v[30:31], v[74:75], v[30:31] neg_lo:[0,1] neg_hi:[0,1]
	v_pk_mul_f32 v[74:75], v[88:89], v[30:31] op_sel:[0,1] op_sel_hi:[0,0] neg_lo:[0,1]
	v_pk_fma_f32 v[30:31], v[88:89], v[30:31], v[74:75] op_sel_hi:[0,1,1]
	v_pk_add_f32 v[74:75], v[72:73], v[56:57]
	v_pk_add_f32 v[56:57], v[72:73], v[56:57] neg_lo:[0,1] neg_hi:[0,1]
	v_sub_f32_e32 v22, v17, v22
	v_pk_mul_f32 v[72:73], v[86:87], v[56:57] op_sel:[0,1] op_sel_hi:[0,0] neg_lo:[0,1]
	v_pk_fma_f32 v[72:73], v[90:91], v[56:57], v[72:73] op_sel_hi:[0,1,1]
	v_pk_add_f32 v[56:57], v[70:71], v[52:53]
	v_pk_add_f32 v[52:53], v[70:71], v[52:53] neg_lo:[0,1] neg_hi:[0,1]
	v_ashrrev_i32_e32 v15, 31, v14
	v_pk_mul_f32 v[70:71], v[84:85], v[52:53] op_sel:[0,1] op_sel_hi:[0,0] neg_lo:[0,1]
	v_pk_fma_f32 v[52:53], v[92:93], v[52:53], v[70:71] op_sel_hi:[0,1,1]
	v_pk_add_f32 v[70:71], v[68:69], v[48:49]
	v_pk_add_f32 v[48:49], v[68:69], v[48:49] neg_lo:[0,1] neg_hi:[0,1]
	v_lshl_add_u64 v[14:15], v[14:15], 2, s[72:73]
	v_pk_mul_f32 v[68:69], v[10:11], v[48:49] op_sel:[0,1] op_sel_hi:[0,0] neg_lo:[0,1]
	v_pk_fma_f32 v[98:99], v[94:95], v[48:49], v[68:69] op_sel_hi:[0,1,1]
	v_pk_add_f32 v[48:49], v[62:63], v[42:43]
	v_pk_add_f32 v[42:43], v[62:63], v[42:43] neg_lo:[0,1] neg_hi:[0,1]
	v_pk_add_f32 v[68:69], v[58:59], v[36:37]
	v_pk_mul_f32 v[62:63], v[10:11], v[42:43] op_sel:[0,1] op_sel_hi:[0,0] neg_lo:[0,1]
	v_pk_fma_f32 v[62:63], v[94:95], v[42:43], v[62:63] op_sel_hi:[0,1,1] neg_lo:[1,0,0] neg_hi:[1,0,0]
	v_pk_add_f32 v[42:43], v[60:61], v[40:41]
	v_pk_add_f32 v[40:41], v[60:61], v[40:41] neg_lo:[0,1] neg_hi:[0,1]
	v_pk_add_f32 v[36:37], v[58:59], v[36:37] neg_lo:[0,1] neg_hi:[0,1]
	v_pk_mul_f32 v[60:61], v[84:85], v[40:41] op_sel:[0,1] op_sel_hi:[0,0] neg_lo:[0,1]
	v_pk_fma_f32 v[60:61], v[92:93], v[40:41], v[60:61] op_sel_hi:[0,1,1] neg_lo:[1,0,0] neg_hi:[1,0,0]
	v_pk_mul_f32 v[40:41], v[86:87], v[36:37] op_sel:[0,1] op_sel_hi:[0,0] neg_lo:[0,1]
	v_pk_fma_f32 v[100:101], v[90:91], v[36:37], v[40:41] op_sel_hi:[0,1,1] neg_lo:[1,0,0] neg_hi:[1,0,0]
	v_pk_add_f32 v[40:41], v[54:55], v[34:35]
	v_pk_add_f32 v[34:35], v[54:55], v[34:35] neg_lo:[0,1] neg_hi:[0,1]
	v_add_f32_e32 v38, v38, v40
	v_pk_mul_f32 v[36:37], v[88:89], v[34:35] op_sel:[0,1] op_sel_hi:[0,0] neg_lo:[0,1]
	v_pk_fma_f32 v[34:35], v[88:89], v[34:35], v[36:37] op_sel_hi:[0,1,1] neg_lo:[1,0,0] neg_hi:[1,0,0]
	v_pk_add_f32 v[36:37], v[50:51], v[32:33]
	v_pk_add_f32 v[32:33], v[50:51], v[32:33] neg_lo:[0,1] neg_hi:[0,1]
	v_add_f32_e32 v30, v30, v34
	v_pk_mul_f32 v[50:51], v[90:91], v[32:33] op_sel:[0,1] op_sel_hi:[0,0] neg_lo:[0,1]
	v_pk_fma_f32 v[86:87], v[86:87], v[32:33], v[50:51] op_sel_hi:[0,1,1] neg_lo:[1,0,0] neg_hi:[1,0,0]
	v_pk_add_f32 v[32:33], v[46:47], v[28:29]
	v_pk_add_f32 v[28:29], v[46:47], v[28:29] neg_lo:[0,1] neg_hi:[0,1]
	v_pk_add_f32 v[50:51], v[44:45], v[26:27]
	v_pk_mul_f32 v[46:47], v[92:93], v[28:29] op_sel:[0,1] op_sel_hi:[0,0] neg_lo:[0,1]
	v_pk_add_f32 v[26:27], v[44:45], v[26:27] neg_lo:[0,1] neg_hi:[0,1]
	v_pk_fma_f32 v[46:47], v[84:85], v[28:29], v[46:47] op_sel_hi:[0,1,1] neg_lo:[1,0,0] neg_hi:[1,0,0]
	v_pk_mul_f32 v[28:29], v[94:95], v[26:27] op_sel:[0,1] op_sel_hi:[0,0] neg_lo:[0,1]
	v_pk_fma_f32 v[90:91], v[10:11], v[26:27], v[28:29] op_sel_hi:[0,1,1] neg_lo:[1,0,0] neg_hi:[1,0,0]
	v_pk_add_f32 v[28:29], v[96:97], v[48:49] neg_lo:[0,1] neg_hi:[0,1]
	v_pk_add_f32 v[26:27], v[96:97], v[48:49]
	v_pk_mul_f32 v[44:45], v[92:93], v[28:29] op_sel:[0,1] op_sel_hi:[0,0] neg_lo:[0,1]
	v_pk_fma_f32 v[94:95], v[84:85], v[28:29], v[44:45] op_sel_hi:[0,1,1]
	v_pk_add_f32 v[28:29], v[66:67], v[42:43] neg_lo:[0,1] neg_hi:[0,1]
	v_pk_add_f32 v[44:45], v[78:79], v[68:69] neg_lo:[0,1] neg_hi:[0,1]
	v_pk_add_f32 v[48:49], v[66:67], v[42:43]
	v_pk_mul_f32 v[42:43], v[88:89], v[28:29] op_sel:[0,1] op_sel_hi:[0,0] neg_lo:[0,1]
	v_pk_mul_f32 v[54:55], v[84:85], v[44:45] op_sel:[0,1] op_sel_hi:[0,0] neg_lo:[0,1]
	v_pk_fma_f32 v[28:29], v[88:89], v[28:29], v[42:43] op_sel_hi:[0,1,1]
	v_pk_add_f32 v[42:43], v[78:79], v[68:69]
	v_pk_fma_f32 v[68:69], v[92:93], v[44:45], v[54:55] op_sel_hi:[0,1,1]
	v_pk_add_f32 v[54:55], v[74:75], v[36:37]
	v_pk_add_f32 v[36:37], v[74:75], v[36:37] neg_lo:[0,1] neg_hi:[0,1]
	v_pk_add_f32 v[58:59], v[56:57], v[32:33]
	v_pk_mul_f32 v[44:45], v[84:85], v[36:37] op_sel:[0,1] op_sel_hi:[0,0] neg_lo:[0,1]
	v_pk_add_f32 v[32:33], v[56:57], v[32:33] neg_lo:[0,1] neg_hi:[0,1]
	v_pk_fma_f32 v[74:75], v[92:93], v[36:37], v[44:45] op_sel_hi:[0,1,1] neg_lo:[1,0,0] neg_hi:[1,0,0]
	v_pk_mul_f32 v[36:37], v[88:89], v[32:33] op_sel:[0,1] op_sel_hi:[0,0] neg_lo:[0,1]
	v_pk_fma_f32 v[44:45], v[88:89], v[32:33], v[36:37] op_sel_hi:[0,1,1] neg_lo:[1,0,0] neg_hi:[1,0,0]
	v_pk_add_f32 v[36:37], v[70:71], v[50:51] neg_lo:[0,1] neg_hi:[0,1]
	v_pk_add_f32 v[32:33], v[70:71], v[50:51]
	v_pk_mul_f32 v[50:51], v[92:93], v[36:37] op_sel:[0,1] op_sel_hi:[0,0] neg_lo:[0,1]
	v_pk_add_f32 v[66:67], v[26:27], v[54:55]
	v_pk_add_f32 v[26:27], v[26:27], v[54:55] neg_lo:[0,1] neg_hi:[0,1]
	v_pk_fma_f32 v[50:51], v[84:85], v[36:37], v[50:51] op_sel_hi:[0,1,1] neg_lo:[1,0,0] neg_hi:[1,0,0]
	v_pk_mul_f32 v[36:37], v[88:89], v[26:27] op_sel:[0,1] op_sel_hi:[0,0] neg_lo:[0,1]
	v_pk_add_f32 v[70:71], v[42:43], v[32:33]
	v_pk_add_f32 v[32:33], v[42:43], v[32:33] neg_lo:[0,1] neg_hi:[0,1]
	v_pk_fma_f32 v[26:27], v[88:89], v[26:27], v[36:37] op_sel_hi:[0,1,1]
	v_pk_mul_f32 v[36:37], v[88:89], v[32:33] op_sel:[0,1] op_sel_hi:[0,0] neg_lo:[0,1]
	v_pk_fma_f32 v[36:37], v[88:89], v[32:33], v[36:37] op_sel_hi:[0,1,1] neg_lo:[1,0,0] neg_hi:[1,0,0]
	v_pk_add_f32 v[32:33], v[94:95], v[74:75] neg_lo:[0,1] neg_hi:[0,1]
	v_pk_add_f32 v[56:57], v[68:69], v[50:51]
	v_pk_mul_f32 v[42:43], v[88:89], v[32:33] op_sel:[0,1] op_sel_hi:[0,0] neg_lo:[0,1]
	v_pk_fma_f32 v[32:33], v[88:89], v[32:33], v[42:43] op_sel_hi:[0,1,1]
	v_pk_add_f32 v[42:43], v[68:69], v[50:51] neg_lo:[0,1] neg_hi:[0,1]
	v_pk_add_f32 v[54:55], v[94:95], v[74:75]
	v_pk_mul_f32 v[50:51], v[88:89], v[42:43] op_sel:[0,1] op_sel_hi:[0,0] neg_lo:[0,1]
	v_pk_fma_f32 v[42:43], v[88:89], v[42:43], v[50:51] op_sel_hi:[0,1,1] neg_lo:[1,0,0] neg_hi:[1,0,0]
	v_pk_add_f32 v[50:51], v[80:81], v[62:63] neg_lo:[0,1] neg_hi:[0,1]
	v_pk_add_f32 v[74:75], v[80:81], v[62:63]
	v_pk_mul_f32 v[62:63], v[92:93], v[50:51] op_sel:[0,1] op_sel_hi:[0,0] neg_lo:[0,1]
	v_pk_fma_f32 v[94:95], v[84:85], v[50:51], v[62:63] op_sel_hi:[0,1,1]
	v_pk_add_f32 v[50:51], v[64:65], v[60:61] neg_lo:[0,1] neg_hi:[0,1]
	v_pk_add_f32 v[68:69], v[64:65], v[60:61]
	v_pk_mul_f32 v[60:61], v[88:89], v[50:51] op_sel:[0,1] op_sel_hi:[0,0] neg_lo:[0,1]
	v_pk_fma_f32 v[50:51], v[88:89], v[50:51], v[60:61] op_sel_hi:[0,1,1]
	v_pk_add_f32 v[60:61], v[76:77], v[100:101] neg_lo:[0,1] neg_hi:[0,1]
	v_pk_add_f32 v[64:65], v[76:77], v[100:101]
	v_pk_mul_f32 v[62:63], v[84:85], v[60:61] op_sel:[0,1] op_sel_hi:[0,0] neg_lo:[0,1]
	v_pk_fma_f32 v[96:97], v[92:93], v[60:61], v[62:63] op_sel_hi:[0,1,1]
	v_pk_add_f32 v[60:61], v[72:73], v[86:87] neg_lo:[0,1] neg_hi:[0,1]
	v_pk_add_f32 v[76:77], v[52:53], v[46:47]
	v_pk_add_f32 v[46:47], v[52:53], v[46:47] neg_lo:[0,1] neg_hi:[0,1]
	v_pk_add_f32 v[62:63], v[72:73], v[86:87]
	v_pk_mul_f32 v[72:73], v[84:85], v[60:61] op_sel:[0,1] op_sel_hi:[0,0] neg_lo:[0,1]
	v_pk_mul_f32 v[52:53], v[88:89], v[46:47] op_sel:[0,1] op_sel_hi:[0,0] neg_lo:[0,1]
	v_pk_fma_f32 v[86:87], v[92:93], v[60:61], v[72:73] op_sel_hi:[0,1,1] neg_lo:[1,0,0] neg_hi:[1,0,0]
	v_pk_fma_f32 v[60:61], v[88:89], v[46:47], v[52:53] op_sel_hi:[0,1,1] neg_lo:[1,0,0] neg_hi:[1,0,0]
	v_pk_add_f32 v[46:47], v[98:99], v[90:91]
	v_pk_add_f32 v[52:53], v[98:99], v[90:91] neg_lo:[0,1] neg_hi:[0,1]
	v_pk_add_f32 v[80:81], v[64:65], v[46:47]
	v_pk_add_f32 v[46:47], v[64:65], v[46:47] neg_lo:[0,1] neg_hi:[0,1]
	v_pk_mul_f32 v[64:65], v[88:89], v[46:47] op_sel:[0,1] op_sel_hi:[0,0] neg_lo:[0,1]
	v_pk_fma_f32 v[64:65], v[88:89], v[46:47], v[64:65] op_sel_hi:[0,1,1] neg_lo:[1,0,0] neg_hi:[1,0,0]
	v_pk_add_f32 v[46:47], v[94:95], v[86:87] neg_lo:[0,1] neg_hi:[0,1]
	v_pk_mul_f32 v[72:73], v[92:93], v[52:53] op_sel:[0,1] op_sel_hi:[0,0] neg_lo:[0,1]
	v_pk_add_f32 v[78:79], v[74:75], v[62:63]
	v_pk_add_f32 v[62:63], v[74:75], v[62:63] neg_lo:[0,1] neg_hi:[0,1]
	v_pk_fma_f32 v[52:53], v[84:85], v[52:53], v[72:73] op_sel_hi:[0,1,1] neg_lo:[1,0,0] neg_hi:[1,0,0]
	v_pk_mul_f32 v[74:75], v[88:89], v[46:47] op_sel:[0,1] op_sel_hi:[0,0] neg_lo:[0,1]
	v_pk_fma_f32 v[46:47], v[88:89], v[46:47], v[74:75] op_sel_hi:[0,1,1]
	v_pk_add_f32 v[74:75], v[96:97], v[52:53]
	v_pk_add_f32 v[52:53], v[96:97], v[52:53] neg_lo:[0,1] neg_hi:[0,1]
	v_sub_f32_e32 v34, v16, v18
	v_pk_mul_f32 v[84:85], v[88:89], v[52:53] op_sel:[0,1] op_sel_hi:[0,0] neg_lo:[0,1]
	v_sub_f32_e32 v25, v33, v43
	v_sub_f32_e32 v43, v31, v35
	v_sub_f32_e32 v35, v51, v61
	v_pk_fma_f32 v[52:53], v[88:89], v[52:53], v[84:85] op_sel_hi:[0,1,1] neg_lo:[1,0,0] neg_hi:[1,0,0]
	v_sub_f32_e32 v51, v34, v82
	v_sub_f32_e32 v13, v49, v59
	v_sub_f32_e32 v10, v47, v53
	v_add_f32_e32 v49, v68, v76
	v_add_f32_e32 v53, v51, v30
	v_sub_f32_e32 v23, v27, v37
	v_sub_f32_e32 v27, v55, v57
	v_add_f32_e32 v40, v78, v80
	v_add_f32_e32 v55, v53, v49
	v_add_f32_e32 v16, v55, v40
	v_sub_f32_e32 v41, v39, v41
	v_add_f32_e32 v48, v48, v58
	v_add_f32_e32 v21, v20, v38
	global_store_dword v[14:15], v16, off offset:2048
	v_add_co_u32_e32 v16, vcc, s85, v14
	v_add_f32_e32 v47, v66, v70
	v_add_f32_e32 v24, v21, v48
	v_add_f32_e32 v28, v28, v44
	v_sub_f32_e32 v44, v22, v41
	v_addc_co_u32_e32 v17, vcc, 0, v15, vcc
	v_pk_mul_f32 v[72:73], v[88:89], v[62:63] op_sel:[0,1] op_sel_hi:[0,0] neg_lo:[0,1]
	v_add_f32_e32 v19, v24, v47
	v_add_f32_e32 v54, v54, v56
	v_add_f32_e32 v56, v44, v28
	v_add_co_u32_e32 v18, vcc, s84, v14
	v_add_f32_e32 v34, v34, v82
	v_pk_fma_f32 v[62:63], v[88:89], v[62:63], v[72:73] op_sel_hi:[0,1,1]
	v_pk_add_f32 v[72:73], v[94:95], v[86:87]
	global_store_dword v[14:15], v19, off
	v_add_f32_e32 v57, v56, v54
	v_addc_co_u32_e32 v19, vcc, 0, v15, vcc
	v_add_f32_e32 v50, v50, v60
	v_sub_f32_e32 v58, v34, v43
	global_store_dword v[18:19], v57, off offset:-4096
	v_add_f32_e32 v57, v72, v74
	v_add_f32_e32 v59, v58, v50
	v_sub_f32_e32 v20, v20, v38
	v_sub_f32_e32 v37, v29, v45
	v_sub_f32_e32 v45, v69, v77
	v_add_f32_e32 v60, v59, v57
	v_add_f32_e32 v26, v26, v36
	v_sub_f32_e32 v36, v20, v13
	v_sub_f32_e32 v30, v51, v30
	global_store_dword v[16:17], v60, off offset:2048
	v_add_f32_e32 v16, v36, v26
	v_add_f32_e32 v38, v62, v64
	v_sub_f32_e32 v51, v30, v45
	global_store_dword v[18:19], v16, off
	v_add_f32_e32 v16, v51, v38
	global_store_dword v[18:19], v16, off offset:2048
	v_add_co_u32_e32 v16, vcc, s61, v14
	v_add_f32_e32 v22, v22, v41
	s_nop 0
	v_addc_co_u32_e32 v17, vcc, 0, v15, vcc
	v_add_f32_e32 v32, v32, v42
	v_sub_f32_e32 v41, v22, v37
	v_add_co_u32_e32 v18, vcc, s45, v14
	v_add_f32_e32 v42, v41, v32
	s_nop 0
	v_addc_co_u32_e32 v19, vcc, 0, v15, vcc
	v_add_f32_e32 v34, v34, v43
	global_store_dword v[18:19], v42, off offset:-4096
	v_add_f32_e32 v42, v46, v52
	v_sub_f32_e32 v43, v34, v35
	v_sub_f32_e32 v39, v67, v71
	v_add_f32_e32 v46, v43, v42
	v_sub_f32_e32 v21, v21, v48
	v_sub_f32_e32 v33, v79, v81
	global_store_dword v[16:17], v46, off offset:2048
	v_sub_f32_e32 v16, v21, v39
	v_sub_f32_e32 v46, v53, v49
	global_store_dword v[18:19], v16, off
	v_sub_f32_e32 v16, v46, v33
	global_store_dword v[18:19], v16, off offset:2048
	v_add_co_u32_e32 v16, vcc, s86, v14
	v_sub_f32_e32 v28, v44, v28
	s_nop 0
	v_addc_co_u32_e32 v17, vcc, 0, v15, vcc
	v_add_co_u32_e32 v18, vcc, s88, v14
	v_sub_f32_e32 v44, v28, v27
	s_nop 0
	v_addc_co_u32_e32 v19, vcc, 0, v15, vcc
	v_sub_f32_e32 v31, v73, v75
	global_store_dword v[18:19], v44, off offset:-4096
	v_sub_f32_e32 v44, v58, v50
	v_sub_f32_e32 v48, v44, v31
	v_add_f32_e32 v20, v20, v13
	v_sub_f32_e32 v29, v63, v65
	global_store_dword v[16:17], v48, off offset:2048
	v_sub_f32_e32 v13, v20, v23
	v_add_f32_e32 v30, v30, v45
	v_add_co_u32_e32 v16, vcc, s90, v14
	global_store_dword v[18:19], v13, off
	v_sub_f32_e32 v13, v30, v29
	v_addc_co_u32_e32 v17, vcc, 0, v15, vcc
	global_store_dword v[18:19], v13, off offset:2048
	v_add_f32_e32 v22, v22, v37
	v_add_co_u32_e32 v18, vcc, s8, v14
	v_sub_f32_e32 v13, v22, v25
	s_nop 0
	v_addc_co_u32_e32 v19, vcc, 0, v15, vcc
	global_store_dword v[18:19], v13, off offset:-4096
	v_add_f32_e32 v13, v34, v35
	v_sub_f32_e32 v34, v13, v10
	global_store_dword v[16:17], v34, off offset:2048
	v_sub_f32_e32 v16, v24, v47
	global_store_dword v[18:19], v16, off
	v_sub_f32_e32 v16, v55, v40
	global_store_dword v[18:19], v16, off offset:2048
	v_add_co_u32_e32 v16, vcc, s9, v14
	v_sub_f32_e32 v24, v56, v54
	s_nop 0
	v_addc_co_u32_e32 v17, vcc, 0, v15, vcc
	v_add_co_u32_e32 v18, vcc, s7, v14
	v_add_f32_e32 v10, v13, v10
	s_nop 0
	v_addc_co_u32_e32 v19, vcc, 0, v15, vcc
	global_store_dword v[18:19], v24, off offset:-4096
	v_sub_f32_e32 v24, v59, v57
	global_store_dword v[16:17], v24, off offset:2048
	v_sub_f32_e32 v16, v36, v26
	global_store_dword v[18:19], v16, off
	v_sub_f32_e32 v16, v51, v38
	global_store_dword v[18:19], v16, off offset:2048
	v_add_co_u32_e32 v16, vcc, s5, v14
	v_sub_f32_e32 v24, v41, v32
	s_nop 0
	v_addc_co_u32_e32 v17, vcc, 0, v15, vcc
	v_add_co_u32_e32 v18, vcc, s6, v14
	s_nop 1
	v_addc_co_u32_e32 v19, vcc, 0, v15, vcc
	global_store_dword v[18:19], v24, off offset:-4096
	v_sub_f32_e32 v24, v43, v42
	global_store_dword v[16:17], v24, off offset:2048
	v_add_f32_e32 v16, v21, v39
	global_store_dword v[18:19], v16, off
	v_add_f32_e32 v16, v46, v33
	global_store_dword v[18:19], v16, off offset:2048
	v_add_co_u32_e32 v16, vcc, s4, v14
	v_add_f32_e32 v21, v28, v27
	s_nop 0
	v_addc_co_u32_e32 v17, vcc, 0, v15, vcc
	v_add_co_u32_e32 v18, vcc, s1, v14
	s_nop 1
	v_addc_co_u32_e32 v19, vcc, 0, v15, vcc
	global_store_dword v[18:19], v21, off offset:-4096
	v_add_f32_e32 v21, v44, v31
	global_store_dword v[16:17], v21, off offset:2048
	v_add_f32_e32 v16, v20, v23
	global_store_dword v[18:19], v16, off
	v_add_f32_e32 v16, v30, v29
	v_add_co_u32_e32 v14, vcc, s0, v14
	global_store_dword v[18:19], v16, off offset:2048
	v_add_f32_e32 v16, v22, v25
	v_addc_co_u32_e32 v15, vcc, 0, v15, vcc
	global_store_dword v[14:15], v16, off
	global_store_dword v[14:15], v10, off offset:2048
	v_mov_b32_e32 v10, v184
	v_mov_b32_e32 v14, v185
	v_mov_b32_e32 v18, v1
	s_movk_i32 s0, 0xfe00
	v_sub_u32_e32 v13, 0x4000, v18
	v_cmp_eq_u32_e32 vcc, 0, v18
	v_cmp_eq_u32_e64 s[0:1], s0, v18
	v_cmp_eq_u32_e64 s[4:5], s50, v18
	v_cndmask_b32_e64 v20, v13, 0, vcc
	v_sub_u32_e32 v13, 0x3e00, v18
	v_cndmask_b32_e64 v22, v13, 0, s[0:1]
	v_sub_u32_e32 v13, 0x3c00, v18
	v_ashrrev_i32_e32 v21, 31, v20
	v_ashrrev_i32_e32 v23, 31, v22
	v_cndmask_b32_e64 v24, v13, 0, s[4:5]
	v_lshl_add_u64 v[20:21], v[20:21], 1, s[2:3]
	v_lshl_add_u64 v[22:23], v[22:23], 1, s[2:3]
	v_ashrrev_i32_e32 v25, 31, v24
	v_sub_u32_e32 v13, 0x3a00, v18
	v_cmp_eq_u32_e64 s[6:7], s51, v18
	v_lshl_add_u64 v[24:25], v[24:25], 1, s[2:3]
	global_load_ushort v15, v[20:21], off
	s_nop 0
	global_load_ushort v22, v[22:23], off
	s_nop 0
	global_load_ushort v23, v[24:25], off
	v_cndmask_b32_e64 v20, v13, 0, s[6:7]
	v_ashrrev_i32_e32 v21, 31, v20
	v_ashrrev_i32_e32 v19, 31, v18
	v_lshl_add_u64 v[20:21], v[20:21], 1, s[2:3]
	v_lshl_add_u64 v[16:17], v[18:19], 1, s[78:79]
	global_load_ushort v20, v[20:21], off
	s_nop 0
	global_load_ushort v13, v[16:17], off offset:3072
	v_sub_u32_e32 v24, 0x3800, v18
	v_sub_u32_e32 v26, 0x3600, v18
	v_sub_u32_e32 v28, 0x3400, v18
	v_sub_u32_e32 v32, 0x3200, v18
	v_cmp_eq_u32_e64 s[8:9], s60, v18
	v_cmp_eq_u32_e64 s[10:11], s10, v18
	s_mov_b32 s78, s69
	s_mov_b32 s79, s68
	s_mov_b32 s50, s21
	s_mov_b32 s51, s20
	s_mov_b32 s60, s25
	s_waitcnt vmcnt(4)
	v_lshlrev_b32_e32 v15, 16, v15
	v_cndmask_b32_e64 v19, -v15, v15, vcc
	s_waitcnt vmcnt(3)
	v_lshlrev_b32_e32 v15, 16, v22
	v_add_co_u32_e32 v22, vcc, s85, v16
	v_cndmask_b32_e64 v31, -v15, v15, s[0:1]
	s_waitcnt vmcnt(2)
	v_lshlrev_b32_e32 v15, 16, v23
	v_addc_co_u32_e32 v23, vcc, 0, v17, vcc
	v_cndmask_b32_e64 v30, -v15, v15, s[4:5]
	s_waitcnt vmcnt(1)
	v_lshlrev_b32_e32 v15, 16, v20
	v_add_co_u32_e32 v20, vcc, s84, v16
	v_cndmask_b32_e64 v15, -v15, v15, s[6:7]
	s_nop 0
	v_addc_co_u32_e32 v21, vcc, 0, v17, vcc
	v_cmp_eq_u32_e64 s[6:7], s56, v18
	v_cmp_eq_u32_e64 s[4:5], s57, v18
	v_cmp_eq_u32_e64 s[0:1], s58, v18
	v_cndmask_b32_e64 v24, v24, 0, s[6:7]
	v_cndmask_b32_e64 v26, v26, 0, s[4:5]
	v_cndmask_b32_e64 v28, v28, 0, s[0:1]
	v_cmp_eq_u32_e32 vcc, s59, v18
	v_ashrrev_i32_e32 v25, 31, v24
	v_ashrrev_i32_e32 v27, 31, v26
	v_ashrrev_i32_e32 v29, 31, v28
	v_cndmask_b32_e64 v32, v32, 0, vcc
	v_lshl_add_u64 v[24:25], v[24:25], 1, s[2:3]
	v_lshl_add_u64 v[26:27], v[26:27], 1, s[2:3]
	v_lshl_add_u64 v[28:29], v[28:29], 1, s[2:3]
	v_ashrrev_i32_e32 v33, 31, v32
	v_lshl_add_u64 v[32:33], v[32:33], 1, s[2:3]
	global_load_ushort v34, v[24:25], off
	s_nop 0
	global_load_ushort v26, v[26:27], off
	s_nop 0
	global_load_ushort v27, v[28:29], off
	s_nop 0
	global_load_ushort v28, v[32:33], off
	v_sub_u32_e32 v24, 0x3000, v18
	v_cndmask_b32_e64 v24, v24, 0, s[8:9]
	v_ashrrev_i32_e32 v25, 31, v24
	v_lshl_add_u64 v[24:25], v[24:25], 1, s[2:3]
	global_load_ushort v24, v[24:25], off
	s_nop 0
	global_load_ushort v33, v[22:23], off offset:3072
	s_waitcnt vmcnt(6)
	v_lshlrev_b32_e32 v13, 16, v13
	s_mov_b32 s56, s39
	s_mov_b32 s57, s38
	s_mov_b32 s58, s19
	s_mov_b32 s59, s18
	s_waitcnt vmcnt(5)
	v_lshlrev_b32_e32 v25, 16, v34
	v_cndmask_b32_e64 v32, -v25, v25, s[6:7]
	s_waitcnt vmcnt(4)
	v_lshlrev_b32_e32 v25, 16, v26
	v_cndmask_b32_e64 v36, -v25, v25, s[4:5]
	s_waitcnt vmcnt(3)
	v_lshlrev_b32_e32 v25, 16, v27
	v_cndmask_b32_e64 v37, -v25, v25, s[0:1]
	v_add_co_u32_e64 v26, s[0:1], s61, v16
	s_waitcnt vmcnt(2)
	v_lshlrev_b32_e32 v25, 16, v28
	s_waitcnt vmcnt(1)
	v_lshlrev_b32_e32 v24, 16, v24
	v_addc_co_u32_e64 v27, s[0:1], 0, v17, s[0:1]
	v_cndmask_b32_e64 v35, -v25, v25, vcc
	v_cndmask_b32_e64 v34, -v24, v24, s[8:9]
	v_sub_u32_e32 v24, 0x2e00, v18
	v_cmp_eq_u32_e32 vcc, s62, v18
	v_sub_u32_e32 v28, 0x2c00, v18
	v_cmp_eq_u32_e64 s[0:1], s63, v18
	v_cndmask_b32_e64 v24, v24, 0, vcc
	v_ashrrev_i32_e32 v25, 31, v24
	v_cndmask_b32_e64 v28, v28, 0, s[0:1]
	v_ashrrev_i32_e32 v29, 31, v28
	v_lshl_add_u64 v[24:25], v[24:25], 1, s[2:3]
	v_lshl_add_u64 v[28:29], v[28:29], 1, s[2:3]
	global_load_ushort v38, v[24:25], off
	s_nop 0
	global_load_ushort v28, v[28:29], off
	v_sub_u32_e32 v24, 0x2a00, v18
	v_cmp_eq_u32_e64 s[4:5], s64, v18
	v_cmp_eq_u32_e64 s[6:7], s65, v18
	s_mov_b32 s62, s29
	v_cndmask_b32_e64 v24, v24, 0, s[4:5]
	v_ashrrev_i32_e32 v25, 31, v24
	v_lshl_add_u64 v[24:25], v[24:25], 1, s[2:3]
	global_load_ushort v29, v[24:25], off
	v_sub_u32_e32 v24, 0x2800, v18
	v_cndmask_b32_e64 v24, v24, 0, s[6:7]
	v_ashrrev_i32_e32 v25, 31, v24
	v_lshl_add_u64 v[24:25], v[24:25], 1, s[2:3]
	global_load_ushort v41, v[26:27], off offset:1024
	global_load_ushort v40, v[26:27], off offset:2048
	global_load_ushort v39, v[26:27], off offset:3072
	global_load_ushort v42, v[24:25], off
	v_sub_u32_e32 v26, 0x2600, v18
	s_mov_b32 s63, s28
	s_mov_b32 s61, s24
	s_waitcnt vmcnt(6)
	v_lshlrev_b32_e32 v24, 16, v38
	v_cndmask_b32_e64 v45, -v24, v24, vcc
	s_waitcnt vmcnt(5)
	v_lshlrev_b32_e32 v24, 16, v28
	v_cndmask_b32_e64 v44, -v24, v24, s[0:1]
	s_movk_i32 s0, 0xe600
	v_sub_u32_e32 v38, 0x2200, v18
	s_waitcnt vmcnt(4)
	v_lshlrev_b32_e32 v24, 16, v29
	v_cndmask_b32_e64 v43, -v24, v24, s[4:5]
	v_add_co_u32_e32 v24, vcc, s45, v16
	s_nop 1
	v_addc_co_u32_e32 v25, vcc, 0, v17, vcc
	v_cmp_eq_u32_e32 vcc, s0, v18
	s_movk_i32 s0, 0xe400
	s_nop 0
	v_cndmask_b32_e64 v26, v26, 0, vcc
	v_ashrrev_i32_e32 v27, 31, v26
	v_lshl_add_u64 v[26:27], v[26:27], 1, s[2:3]
	global_load_ushort v26, v[26:27], off
	s_waitcnt vmcnt(1)
	v_lshlrev_b32_e32 v27, 16, v42
	v_cndmask_b32_e64 v49, -v27, v27, s[6:7]
	s_waitcnt vmcnt(0)
	v_lshlrev_b32_e32 v26, 16, v26
	v_cndmask_b32_e64 v50, -v26, v26, vcc
	v_cmp_eq_u32_e32 vcc, s0, v18
	v_add_co_u32_e64 v28, s[0:1], s86, v16
	v_sub_u32_e32 v26, 0x2400, v18
	s_nop 0
	v_addc_co_u32_e64 v29, s[0:1], 0, v17, s[0:1]
	s_movk_i32 s0, 0xe200
	s_nop 0
	v_cmp_eq_u32_e64 s[8:9], s0, v18
	s_movk_i32 s0, 0xe000
	v_cmp_eq_u32_e64 s[6:7], s0, v18
	v_cndmask_b32_e64 v46, v38, 0, s[8:9]
	v_sub_u32_e32 v38, 0x2000, v18
	s_movk_i32 s0, 0xde00
	v_cndmask_b32_e64 v52, v38, 0, s[6:7]
	v_sub_u32_e32 v38, 0x1e00, v18
	v_cmp_eq_u32_e64 s[4:5], s0, v18
	s_movk_i32 s0, 0xdc00
	v_cndmask_b32_e64 v26, v26, 0, vcc
	v_cndmask_b32_e64 v54, v38, 0, s[4:5]
	v_sub_u32_e32 v38, 0x1c00, v18
	v_cmp_eq_u32_e64 s[0:1], s0, v18
	v_ashrrev_i32_e32 v27, 31, v26
	v_ashrrev_i32_e32 v47, 31, v46
	v_cndmask_b32_e64 v56, v38, 0, s[0:1]
	v_lshl_add_u64 v[26:27], v[26:27], 1, s[2:3]
	v_lshl_add_u64 v[46:47], v[46:47], 1, s[2:3]
	v_ashrrev_i32_e32 v53, 31, v52
	v_ashrrev_i32_e32 v55, 31, v54
	v_ashrrev_i32_e32 v57, 31, v56
	v_lshl_add_u64 v[52:53], v[52:53], 1, s[2:3]
	v_lshl_add_u64 v[54:55], v[54:55], 1, s[2:3]
	v_lshl_add_u64 v[56:57], v[56:57], 1, s[2:3]
	global_load_ushort v38, v[26:27], off
	global_load_ushort v42, v[46:47], off
	s_nop 0
	global_load_ushort v46, v[52:53], off
	global_load_ushort v47, v[54:55], off
	global_load_ushort v48, v[56:57], off
	v_sub_u32_e32 v26, 0x1a00, v18
	v_cndmask_b32_e64 v26, v26, 0, s[10:11]
	v_ashrrev_i32_e32 v27, 31, v26
	v_lshl_add_u64 v[26:27], v[26:27], 1, s[2:3]
	global_load_ushort v26, v[26:27], off
	s_nop 0
	global_load_ushort v53, v[28:29], off offset:1024
	global_load_ushort v51, v[28:29], off offset:2048
	s_waitcnt vmcnt(7)
	v_lshlrev_b32_e32 v27, 16, v38
	v_cndmask_b32_e64 v61, -v27, v27, vcc
	s_waitcnt vmcnt(6)
	v_lshlrev_b32_e32 v27, 16, v42
	v_cndmask_b32_e64 v63, -v27, v27, s[8:9]
	s_waitcnt vmcnt(5)
	v_lshlrev_b32_e32 v27, 16, v46
	v_cndmask_b32_e64 v90, -v27, v27, s[6:7]
	s_waitcnt vmcnt(4)
	v_lshlrev_b32_e32 v27, 16, v47
	v_cndmask_b32_e64 v59, -v27, v27, s[4:5]
	s_waitcnt vmcnt(3)
	v_lshlrev_b32_e32 v27, 16, v48
	v_cndmask_b32_e64 v57, -v27, v27, s[0:1]
	s_movk_i32 s0, 0xd800
	v_sub_u32_e32 v38, 0x1800, v18
	v_cmp_eq_u32_e64 s[8:9], s0, v18
	s_movk_i32 s0, 0xd600
	s_waitcnt vmcnt(2)
	v_lshlrev_b32_e32 v26, 16, v26
	v_cndmask_b32_e64 v46, v38, 0, s[8:9]
	v_sub_u32_e32 v38, 0x1600, v18
	v_cmp_eq_u32_e64 s[6:7], s0, v18
	s_movk_i32 s0, 0xd400
	v_cndmask_b32_e64 v55, -v26, v26, s[10:11]
	v_add_co_u32_e32 v26, vcc, s88, v16
	v_cndmask_b32_e64 v64, v38, 0, s[6:7]
	v_sub_u32_e32 v38, 0x1400, v18
	v_cmp_eq_u32_e64 s[4:5], s0, v18
	s_movk_i32 s0, 0xd200
	v_addc_co_u32_e32 v27, vcc, 0, v17, vcc
	v_cndmask_b32_e64 v66, v38, 0, s[4:5]
	v_sub_u32_e32 v38, 0x1200, v18
	v_cmp_eq_u32_e64 s[0:1], s0, v18
	s_movk_i32 s10, 0xd000
	v_cmp_eq_u32_e32 vcc, s10, v18
	v_cndmask_b32_e64 v68, v38, 0, s[0:1]
	v_sub_u32_e32 v38, 0x1000, v18
	v_ashrrev_i32_e32 v47, 31, v46
	v_cndmask_b32_e64 v70, v38, 0, vcc
	v_lshl_add_u64 v[46:47], v[46:47], 1, s[2:3]
	v_ashrrev_i32_e32 v65, 31, v64
	v_ashrrev_i32_e32 v67, 31, v66
	v_ashrrev_i32_e32 v69, 31, v68
	v_ashrrev_i32_e32 v71, 31, v70
	s_movk_i32 s10, 0xce00
	v_lshl_add_u64 v[64:65], v[64:65], 1, s[2:3]
	v_lshl_add_u64 v[66:67], v[66:67], 1, s[2:3]
	v_lshl_add_u64 v[68:69], v[68:69], 1, s[2:3]
	v_lshl_add_u64 v[70:71], v[70:71], 1, s[2:3]
	global_load_ushort v38, v[46:47], off
	global_load_ushort v42, v[64:65], off
	global_load_ushort v48, v[66:67], off
	global_load_ushort v52, v[68:69], off
	global_load_ushort v54, v[70:71], off
	v_sub_u32_e32 v46, 0xe00, v18
	v_cmp_eq_u32_e64 s[12:13], s10, v18
	s_movk_i32 s10, 0xcc00
	v_cmp_eq_u32_e64 s[10:11], s10, v18
	v_cndmask_b32_e64 v46, v46, 0, s[12:13]
	v_ashrrev_i32_e32 v47, 31, v46
	v_lshl_add_u64 v[46:47], v[46:47], 1, s[2:3]
	global_load_ushort v56, v[46:47], off
	v_sub_u32_e32 v46, 0xc00, v18
	v_cndmask_b32_e64 v46, v46, 0, s[10:11]
	v_ashrrev_i32_e32 v47, 31, v46
	v_lshl_add_u64 v[46:47], v[46:47], 1, s[2:3]
	global_load_ushort v46, v[46:47], off
	s_nop 0
	global_load_ushort v91, v[28:29], off offset:3072
	s_waitcnt vmcnt(7)
	v_lshlrev_b32_e32 v28, 16, v38
	v_cndmask_b32_e64 v97, -v28, v28, s[8:9]
	s_waitcnt vmcnt(6)
	v_lshlrev_b32_e32 v28, 16, v42
	v_cndmask_b32_e64 v96, -v28, v28, s[6:7]
	s_waitcnt vmcnt(5)
	v_lshlrev_b32_e32 v28, 16, v48
	v_cndmask_b32_e64 v94, -v28, v28, s[4:5]
	s_waitcnt vmcnt(4)
	v_lshlrev_b32_e32 v28, 16, v52
	v_cndmask_b32_e64 v93, -v28, v28, s[0:1]
	s_waitcnt vmcnt(3)
	v_lshlrev_b32_e32 v28, 16, v54
	v_cndmask_b32_e64 v92, -v28, v28, vcc
	s_movk_i32 s0, 0xca00
	v_cmp_eq_u32_e64 s[0:1], s0, v18
	s_waitcnt vmcnt(2)
	v_lshlrev_b32_e32 v28, 16, v56
	v_cndmask_b32_e64 v95, -v28, v28, s[12:13]
	v_sub_u32_e32 v28, 0xa00, v18
	v_cndmask_b32_e64 v28, v28, 0, s[0:1]
	v_ashrrev_i32_e32 v29, 31, v28
	v_lshl_add_u64 v[28:29], v[28:29], 1, s[2:3]
	global_load_ushort v38, v[28:29], off
	s_waitcnt vmcnt(2)
	v_lshlrev_b32_e32 v28, 16, v46
	v_cndmask_b32_e64 v106, -v28, v28, s[10:11]
	v_add_co_u32_e32 v28, vcc, s90, v16
	s_movk_i32 s4, 0xc400
	s_nop 0
	v_addc_co_u32_e32 v29, vcc, 0, v17, vcc
	v_sub_u32_e32 v42, 0x400, v18
	v_cmp_eq_u32_e32 vcc, s4, v18
	s_movk_i32 s4, 0xc800
	v_cmp_eq_u32_e64 s[4:5], s4, v18
	v_cndmask_b32_e64 v46, v42, 0, vcc
	v_sub_u32_e32 v42, 0x800, v18
	v_ashrrev_i32_e32 v47, 31, v46
	v_cndmask_b32_e64 v64, v42, 0, s[4:5]
	v_lshl_add_u64 v[46:47], v[46:47], 1, s[2:3]
	v_ashrrev_i32_e32 v65, 31, v64
	v_lshl_add_u64 v[64:65], v[64:65], 1, s[2:3]
	global_load_ushort v42, v[46:47], off
	s_nop 0
	global_load_ushort v46, v[64:65], off
	global_load_ushort v110, v[28:29], off
	global_load_ushort v112, v[28:29], off offset:1024
	global_load_ushort v114, v[28:29], off offset:2048
	global_load_ushort v116, v[28:29], off offset:3072
	s_mov_b32 s10, 0x3f74fa0b
	s_mov_b32 s11, 0xbe94a031
	s_mov_b32 s80, s11
	s_mov_b32 s81, s10
	v_add_f32_e32 v52, v15, v13
	s_mov_b32 s12, 0x3e94a031
	s_mov_b32 s13, 0xbf74fa0b
	s_mov_b32 s64, s13
	s_mov_b32 s65, s12
	s_mov_b32 s8, 0x3e47c5c2
	s_mov_b32 s9, 0xbf7b14be
	s_mov_b32 s30, s9
	s_mov_b32 s31, s8
	s_mov_b32 s6, 0x3f7b14be
	s_mov_b32 s7, 0xbe47c5c2
	s_mov_b32 s6, s9
	s_waitcnt vmcnt(6)
	v_lshlrev_b32_e32 v28, 16, v38
	v_cndmask_b32_e64 v108, -v28, v28, s[0:1]
	s_movk_i32 s0, 0xc600
	v_sub_u32_e32 v28, 0x600, v18
	v_sub_u32_e32 v38, 0x200, v18
	s_waitcnt vmcnt(4)
	v_lshlrev_b32_e32 v29, 16, v46
	v_cndmask_b32_e64 v111, -v29, v29, s[4:5]
	v_cmp_eq_u32_e64 s[4:5], s0, v18
	s_movk_i32 s0, 0xc200
	v_cmp_eq_u32_e64 s[0:1], s0, v18
	v_cndmask_b32_e64 v28, v28, 0, s[4:5]
	v_ashrrev_i32_e32 v29, 31, v28
	v_cndmask_b32_e64 v46, v38, 0, s[0:1]
	v_lshl_add_u64 v[28:29], v[28:29], 1, s[2:3]
	v_ashrrev_i32_e32 v47, 31, v46
	v_lshl_add_u64 v[46:47], v[46:47], 1, s[2:3]
	global_load_ushort v18, v[16:17], off
	s_nop 0
	global_load_ushort v28, v[28:29], off
	s_nop 0
	global_load_ushort v29, v[16:17], off offset:1024
	s_nop 0
	global_load_ushort v17, v[16:17], off offset:2048
	s_nop 0
	global_load_ushort v38, v[46:47], off
	global_load_ushort v56, v[20:21], off offset:1024
	global_load_ushort v58, v[20:21], off offset:2048
	global_load_ushort v60, v[20:21], off offset:3072
	global_load_ushort v62, v[24:25], off offset:-4096
	global_load_ushort v98, v[24:25], off
	global_load_ushort v48, v[20:21], off offset:-4096
	global_load_ushort v64, v[22:23], off offset:1024
	global_load_ushort v68, v[22:23], off offset:2048
	s_nop 0
	global_load_ushort v21, v[20:21], off
	v_lshlrev_b32_e32 v22, 16, v42
	v_cndmask_b32_e64 v115, -v22, v22, vcc
	v_pk_mul_f32 v[22:23], v[14:15], s[78:79] op_sel_hi:[0,1] neg_lo:[1,0]
	s_mov_b64 vcc, s[66:67]
	s_mov_b32 s66, s71
	s_mov_b32 s67, s70
	s_mov_b32 s2, 0x3f7ec46d
	s_mov_b32 s3, 0xbdc8bd36
	s_waitcnt vmcnt(13)
	v_lshlrev_b32_e32 v16, 16, v18
	s_waitcnt vmcnt(12)
	v_lshlrev_b32_e32 v18, 16, v28
	s_waitcnt vmcnt(11)
	v_lshlrev_b32_e32 v20, 16, v29
	s_waitcnt vmcnt(10)
	v_lshlrev_b32_e32 v17, 16, v17
	v_add_f32_e32 v20, v31, v20
	v_pk_fma_f32 v[28:29], v[10:11], s[68:69], v[22:23] op_sel_hi:[0,1,1]
	v_add_f32_e32 v22, v30, v17
	v_pk_mul_f32 v[30:31], v[14:15], s[66:67] op_sel_hi:[0,1] neg_lo:[1,0]
	v_pk_fma_f32 v[46:47], v[10:11], s[70:71], v[30:31] op_sel_hi:[0,1,1]
	v_pk_mul_f32 v[30:31], v[14:15], s[80:81] op_sel_hi:[0,1] neg_lo:[1,0]
	v_pk_fma_f32 v[88:89], v[10:11], s[10:11], v[30:31] op_sel_hi:[0,1,1]
	s_waitcnt vmcnt(3)
	v_lshlrev_b32_e32 v13, 16, v48
	v_pk_mul_f32 v[30:31], v[14:15], s[52:53] op_sel_hi:[0,1] neg_lo:[1,0]
	v_add_f32_e32 v16, v19, v16
	v_cndmask_b32_e64 v113, -v18, v18, s[4:5]
	v_pk_mul_f32 v[18:19], v[14:15], s[40:41] op_sel_hi:[0,1] neg_lo:[1,0]
	v_add_f32_e32 v54, v32, v13
	v_pk_fma_f32 v[66:67], v[10:11], s[94:95], v[30:31] op_sel_hi:[0,1,1]
	s_waitcnt vmcnt(2)
	v_lshlrev_b32_e32 v13, 16, v64
	v_pk_mul_f32 v[30:31], v[14:15], s[50:51] op_sel_hi:[0,1] neg_lo:[1,0]
	s_waitcnt vmcnt(1)
	v_lshlrev_b32_e32 v15, 16, v68
	v_lshlrev_b32_e32 v17, 16, v38
	v_add_f32_e32 v32, v36, v13
	global_load_ushort v13, v[24:25], off offset:1024
	v_add_f32_e32 v38, v37, v15
	global_load_ushort v15, v[24:25], off offset:2048
	v_lshlrev_b32_e32 v23, 16, v33
	s_waitcnt vmcnt(2)
	v_lshlrev_b32_e32 v21, 16, v21
	v_add_f32_e32 v42, v35, v23
	global_load_ushort v23, v[24:25], off offset:3072
	global_load_ushort v33, v[26:27], off
	v_add_f32_e32 v48, v34, v21
	v_lshlrev_b32_e32 v21, 16, v56
	v_add_f32_e32 v56, v45, v21
	global_load_ushort v21, v[26:27], off offset:-4096
	s_mov_b32 s68, s83
	s_mov_b32 s69, s82
	s_mov_b32 s70, s23
	s_mov_b32 s71, s22
	v_pk_fma_f32 v[64:65], v[10:11], s[20:21], v[30:31] op_sel_hi:[0,1,1]
	s_mov_b32 s94, s75
	s_mov_b32 s95, s74
	s_mov_b32 s4, 0x3dc8bd36
	s_mov_b32 s5, 0xbf7ec46d
	s_mov_b32 s34, s5
	s_mov_b32 s35, s4
	s_mov_b32 s2, s5
	v_cndmask_b32_e64 v17, -v17, v17, s[0:1]
	s_mov_b32 s0, s3
	s_mov_b32 s1, s5
	s_mov_b32 s10, s13
	s_mov_b32 s20, s23
	v_pk_fma_f32 v[18:19], v[10:11], s[46:47], v[18:19] op_sel_hi:[0,1,1]
	s_waitcnt vmcnt(4)
	v_lshlrev_b32_e32 v13, 16, v13
	s_waitcnt vmcnt(3)
	v_pk_mul_f32 v[24:25], v[14:15], s[56:57] op_sel_hi:[0,1] neg_lo:[1,0]
	v_pk_fma_f32 v[76:77], v[10:11], s[38:39], v[24:25] op_sel_hi:[0,1,1]
	v_pk_mul_f32 v[24:25], v[14:15], s[62:63] op_sel_hi:[0,1] neg_lo:[1,0]
	v_pk_fma_f32 v[82:83], v[10:11], s[28:29], v[24:25] op_sel_hi:[0,1,1]
	v_lshlrev_b32_e32 v24, 16, v58
	v_add_f32_e32 v58, v44, v24
	v_pk_mul_f32 v[24:25], v[14:15], s[68:69] op_sel_hi:[0,1] neg_lo:[1,0]
	v_pk_fma_f32 v[84:85], v[10:11], s[82:83], v[24:25] op_sel_hi:[0,1,1]
	v_lshlrev_b32_e32 v24, 16, v60
	v_add_f32_e32 v60, v43, v24
	v_pk_mul_f32 v[24:25], v[14:15], s[70:71] op_sel_hi:[0,1] neg_lo:[1,0]
	v_pk_fma_f32 v[86:87], v[10:11], s[22:23], v[24:25] op_sel_hi:[0,1,1]
	v_lshlrev_b32_e32 v24, 16, v62
	v_add_f32_e32 v62, v49, v24
	v_pk_mul_f32 v[24:25], v[14:15], s[58:59] op_sel_hi:[0,1] neg_lo:[1,0]
	v_pk_fma_f32 v[80:81], v[10:11], s[18:19], v[24:25] op_sel_hi:[0,1,1]
	v_lshlrev_b32_e32 v24, 16, v41
	v_add_f32_e32 v50, v50, v24
	v_pk_mul_f32 v[24:25], v[14:15], s[64:65] op_sel_hi:[0,1] neg_lo:[1,0]
	v_pk_fma_f32 v[78:79], v[10:11], s[12:13], v[24:25] op_sel_hi:[0,1,1]
	v_lshlrev_b32_e32 v25, 16, v39
	v_add_f32_e32 v44, v63, v25
	global_load_ushort v25, v[26:27], off offset:1024
	global_load_ushort v39, v[26:27], off offset:2048
	v_lshlrev_b32_e32 v24, 16, v40
	global_load_ushort v40, v[26:27], off offset:3072
	v_pk_mul_f32 v[30:31], v[14:15], s[60:61] op_sel_hi:[0,1] neg_lo:[1,0]
	v_pk_fma_f32 v[68:69], v[10:11], s[24:25], v[30:31] op_sel_hi:[0,1,1]
	v_pk_mul_f32 v[30:31], v[14:15], s[94:95] op_sel_hi:[0,1] neg_lo:[1,0]
	v_pk_fma_f32 v[74:75], v[10:11], s[74:75], v[30:31] op_sel_hi:[0,1,1]
	v_pk_mul_f32 v[30:31], v[14:15], s[30:31] op_sel_hi:[0,1] neg_lo:[1,0]
	v_pk_fma_f32 v[70:71], v[10:11], s[8:9], v[30:31] op_sel_hi:[0,1,1]
	v_pk_mul_f32 v[30:31], v[14:15], s[34:35] op_sel_hi:[0,1] neg_lo:[1,0]
	v_pk_fma_f32 v[72:73], v[10:11], s[4:5], v[30:31] op_sel_hi:[0,1,1]
	v_lshlrev_b32_e32 v30, 16, v98
	v_pk_mul_f32 v[34:35], v[14:15], s[36:37] op_sel_hi:[0,1] neg_lo:[1,0]
	v_add_f32_e32 v30, v90, v30
	v_pk_fma_f32 v[34:35], v[10:11], s[76:77], v[34:35] op_sel_hi:[0,1,1]
	v_pk_mul_f32 v[36:37], v[34:35], v[30:31] op_sel_hi:[1,0]
	v_pk_mul_f32 v[30:31], v[14:15], s[2:3] op_sel_hi:[0,1] neg_lo:[1,0]
	v_add_f32_e32 v26, v59, v13
	v_pk_fma_f32 v[30:31], v[10:11], s[0:1], v[30:31] op_sel_hi:[0,1,1]
	v_lshlrev_b32_e32 v13, 16, v15
	s_mov_b32 s4, s7
	s_mov_b32 s5, s9
	v_pk_mul_f32 v[34:35], v[14:15], s[6:7] op_sel_hi:[0,1] neg_lo:[1,0]
	v_pk_mul_f32 v[26:27], v[30:31], v[26:27] op_sel_hi:[1,0]
	v_add_f32_e32 v30, v57, v13
	v_pk_fma_f32 v[34:35], v[10:11], s[4:5], v[34:35] op_sel_hi:[0,1,1]
	v_pk_mul_f32 v[98:99], v[34:35], v[30:31] op_sel_hi:[1,0]
	s_waitcnt vmcnt(5)
	v_lshlrev_b32_e32 v13, 16, v23
	s_mov_b32 s8, s11
	s_mov_b32 s9, s13
	v_pk_mul_f32 v[34:35], v[14:15], s[10:11] op_sel_hi:[0,1] neg_lo:[1,0]
	v_add_f32_e32 v30, v55, v13
	v_pk_fma_f32 v[34:35], v[10:11], s[8:9], v[34:35] op_sel_hi:[0,1,1]
	v_pk_mul_f32 v[100:101], v[34:35], v[30:31] op_sel_hi:[1,0]
	s_waitcnt vmcnt(3)
	v_lshlrev_b32_e32 v13, 16, v21
	s_mov_b32 s12, s17
	s_mov_b32 s13, s19
	v_pk_mul_f32 v[34:35], v[14:15], s[16:17] op_sel_hi:[0,1] neg_lo:[1,0]
	v_add_f32_e32 v30, v97, v13
	v_pk_fma_f32 v[34:35], v[10:11], s[12:13], v[34:35] op_sel_hi:[0,1,1]
	v_pk_mul_f32 v[102:103], v[34:35], v[30:31] op_sel_hi:[1,0]
	v_lshlrev_b32_e32 v13, 16, v53
	s_mov_b32 s18, s21
	s_mov_b32 s19, s23
	v_pk_mul_f32 v[34:35], v[14:15], s[20:21] op_sel_hi:[0,1] neg_lo:[1,0]
	v_add_f32_e32 v30, v96, v13
	v_pk_fma_f32 v[34:35], v[10:11], s[18:19], v[34:35] op_sel_hi:[0,1,1]
	s_mov_b32 s24, s83
	v_pk_mul_f32 v[96:97], v[34:35], v[30:31] op_sel_hi:[1,0]
	v_lshlrev_b32_e32 v13, 16, v51
	s_mov_b32 s22, s25
	s_mov_b32 s23, s83
	v_pk_mul_f32 v[34:35], v[14:15], s[24:25] op_sel_hi:[0,1] neg_lo:[1,0]
	v_add_f32_e32 v30, v94, v13
	v_pk_fma_f32 v[34:35], v[10:11], s[22:23], v[34:35] op_sel_hi:[0,1,1]
	s_mov_b32 s28, s29
	s_mov_b32 s29, s75
	v_pk_mul_f32 v[104:105], v[34:35], v[30:31] op_sel_hi:[1,0]
	v_lshlrev_b32_e32 v13, 16, v91
	v_pk_mul_f32 v[34:35], v[14:15], s[28:29] op_sel_hi:[0,1] neg_lo:[1,0]
	v_add_f32_e32 v30, v93, v13
	v_pk_fma_f32 v[34:35], v[10:11], s[26:27], v[34:35] op_sel_hi:[0,1,1]
	v_pk_mul_f32 v[90:91], v[34:35], v[30:31] op_sel_hi:[1,0]
	v_lshlrev_b32_e32 v13, 16, v33
	v_pk_mul_f32 v[34:35], v[14:15], s[38:39] op_sel_hi:[0,0] neg_lo:[1,0]
	s_mov_b32 s38, s39
	v_add_f32_e32 v30, v92, v13
	v_pk_fma_f32 v[34:35], v[10:11], s[38:39], v[34:35] op_sel_hi:[0,0,1] neg_lo:[0,0,1] neg_hi:[0,0,1]
	v_pk_mul_f32 v[92:93], v[34:35], v[30:31] op_sel_hi:[1,0]
	v_pk_mul_f32 v[34:35], v[14:15], s[26:27] op_sel_hi:[0,1] neg_lo:[1,0]
	v_pk_fma_f32 v[34:35], v[10:11], s[28:29], v[34:35] op_sel_hi:[0,1,1]
	v_add_f32_e32 v24, v61, v24
	s_waitcnt vmcnt(2)
	v_lshlrev_b32_e32 v13, 16, v25
	v_add_f32_e32 v30, v95, v13
	v_pk_mul_f32 v[94:95], v[34:35], v[30:31] op_sel_hi:[1,0]
	s_waitcnt vmcnt(1)
	v_lshlrev_b32_e32 v13, 16, v39
	v_pk_mul_f32 v[34:35], v[14:15], s[22:23] op_sel_hi:[0,1] neg_lo:[1,0]
	v_add_f32_e32 v30, v106, v13
	v_pk_fma_f32 v[34:35], v[10:11], s[24:25], v[34:35] op_sel_hi:[0,1,1]
	v_pk_mul_f32 v[106:107], v[34:35], v[30:31] op_sel_hi:[1,0]
	s_waitcnt vmcnt(0)
	v_lshlrev_b32_e32 v13, 16, v40
	v_pk_mul_f32 v[34:35], v[14:15], s[18:19] op_sel_hi:[0,1] neg_lo:[1,0]
	v_add_f32_e32 v30, v108, v13
	v_pk_fma_f32 v[34:35], v[10:11], s[20:21], v[34:35] op_sel_hi:[0,1,1]
	v_pk_mul_f32 v[108:109], v[34:35], v[30:31] op_sel_hi:[1,0]
	v_lshlrev_b32_e32 v13, 16, v110
	v_pk_mul_f32 v[34:35], v[14:15], s[12:13] op_sel_hi:[0,1] neg_lo:[1,0]
	v_add_f32_e32 v30, v111, v13
	v_pk_fma_f32 v[34:35], v[10:11], s[16:17], v[34:35] op_sel_hi:[0,1,1]
	v_pk_mul_f32 v[110:111], v[34:35], v[30:31] op_sel_hi:[1,0]
	v_lshlrev_b32_e32 v13, 16, v112
	v_pk_mul_f32 v[34:35], v[14:15], s[8:9] op_sel_hi:[0,1] neg_lo:[1,0]
	v_add_f32_e32 v30, v113, v13
	v_pk_fma_f32 v[34:35], v[10:11], s[10:11], v[34:35] op_sel_hi:[0,1,1]
	v_pk_mul_f32 v[112:113], v[34:35], v[30:31] op_sel_hi:[1,0]
	v_lshlrev_b32_e32 v13, 16, v114
	v_pk_mul_f32 v[34:35], v[14:15], s[4:5] op_sel_hi:[0,1] neg_lo:[1,0]
	v_add_f32_e32 v30, v115, v13
	v_pk_fma_f32 v[34:35], v[10:11], s[6:7], v[34:35] op_sel_hi:[0,1,1]
	v_lshlrev_b32_e32 v13, 16, v116
	v_pk_mul_f32 v[14:15], v[14:15], s[0:1] op_sel_hi:[0,1] neg_lo:[1,0]
	v_pk_mul_f32 v[114:115], v[34:35], v[30:31] op_sel_hi:[1,0]
	v_add_f32_e32 v30, v17, v13
	v_pk_fma_f32 v[14:15], v[10:11], s[2:3], v[14:15] op_sel_hi:[0,1,1]
	v_pk_mul_f32 v[116:117], v[14:15], v[30:31] op_sel_hi:[1,0]
	v_mov_b32_e32 v13, v174
	v_mov_b32_e32 v10, v164
	v_mov_b32_e32 v30, v166
	v_mov_b32_e32 v10, v168
	v_mov_b32_e32 v34, v170
	v_mov_b32_e32 v17, v172
	s_nop 0
	v_pk_fma_f32 v[126:127], v[18:19], v[16:17], v[36:37] op_sel_hi:[1,0,1]
	v_pk_fma_f32 v[36:37], v[18:19], v[16:17], v[36:37] op_sel_hi:[1,0,1] neg_lo:[0,0,1] neg_hi:[0,0,1]
	v_pk_fma_f32 v[18:19], v[28:29], v[20:21], v[26:27] op_sel_hi:[1,0,1] neg_lo:[0,0,1] neg_hi:[0,0,1]
	v_pk_fma_f32 v[16:17], v[28:29], v[20:21], v[26:27] op_sel_hi:[1,0,1]
	v_pk_mul_f32 v[20:21], v[18:19], v[124:125] op_sel:[1,0] op_sel_hi:[0,0] neg_lo:[1,1] neg_hi:[0,1]
	v_pk_fma_f32 v[40:41], v[18:19], v[118:119], v[20:21] op_sel_hi:[1,0,1]
	v_pk_fma_f32 v[20:21], v[46:47], v[22:23], v[98:99] op_sel_hi:[1,0,1] neg_lo:[0,0,1] neg_hi:[0,0,1]
	v_pk_fma_f32 v[18:19], v[46:47], v[22:23], v[98:99] op_sel_hi:[1,0,1]
	v_pk_mul_f32 v[22:23], v[20:21], v[34:35] op_sel:[1,0] op_sel_hi:[0,0] neg_lo:[1,1] neg_hi:[0,1]
	v_pk_fma_f32 v[46:47], v[20:21], v[30:31], v[22:23] op_sel_hi:[1,0,1]
	v_pk_fma_f32 v[22:23], v[88:89], v[52:53], v[100:101] op_sel_hi:[1,0,1] neg_lo:[0,0,1] neg_hi:[0,0,1]
	v_pk_fma_f32 v[20:21], v[88:89], v[52:53], v[100:101] op_sel_hi:[1,0,1]
	v_pk_mul_f32 v[26:27], v[22:23], v[122:123] op_sel:[1,0] op_sel_hi:[0,0] neg_lo:[1,1] neg_hi:[0,1]
	v_pk_fma_f32 v[52:53], v[22:23], v[120:121], v[26:27] op_sel_hi:[1,0,1]
	v_pk_fma_f32 v[26:27], v[66:67], v[54:55], v[102:103] op_sel_hi:[1,0,1] neg_lo:[0,0,1] neg_hi:[0,0,1]
	v_pk_fma_f32 v[22:23], v[66:67], v[54:55], v[102:103] op_sel_hi:[1,0,1]
	v_pk_mul_f32 v[28:29], v[26:27], v[10:11] op_sel:[1,0] op_sel_hi:[0,0] neg_lo:[1,1] neg_hi:[0,1]
	v_pk_fma_f32 v[54:55], v[26:27], v[10:11], v[28:29] op_sel_hi:[1,0,1]
	v_pk_fma_f32 v[28:29], v[64:65], v[32:33], v[96:97] op_sel_hi:[1,0,1] neg_lo:[0,0,1] neg_hi:[0,0,1]
	v_pk_fma_f32 v[26:27], v[64:65], v[32:33], v[96:97] op_sel_hi:[1,0,1]
	v_pk_mul_f32 v[32:33], v[28:29], v[122:123] op_sel_hi:[1,0]
	v_pk_fma_f32 v[64:65], v[28:29], v[120:121], v[32:33] op_sel:[1,0,0] op_sel_hi:[0,0,1] neg_lo:[1,1,0] neg_hi:[0,1,0]
	v_pk_fma_f32 v[32:33], v[68:69], v[38:39], v[104:105] op_sel_hi:[1,0,1] neg_lo:[0,0,1] neg_hi:[0,0,1]
	v_pk_fma_f32 v[28:29], v[68:69], v[38:39], v[104:105] op_sel_hi:[1,0,1]
	v_pk_mul_f32 v[38:39], v[32:33], v[34:35] op_sel_hi:[1,0]
	v_pk_fma_f32 v[66:67], v[32:33], v[30:31], v[38:39] op_sel:[1,0,0] op_sel_hi:[0,0,1] neg_lo:[1,1,0] neg_hi:[0,1,0]
	v_pk_fma_f32 v[38:39], v[74:75], v[42:43], v[90:91] op_sel_hi:[1,0,1] neg_lo:[0,0,1] neg_hi:[0,0,1]
	v_pk_fma_f32 v[32:33], v[74:75], v[42:43], v[90:91] op_sel_hi:[1,0,1]
	v_pk_mul_f32 v[42:43], v[38:39], v[124:125] op_sel_hi:[1,0]
	v_pk_fma_f32 v[68:69], v[38:39], v[118:119], v[42:43] op_sel:[1,0,0] op_sel_hi:[0,0,1] neg_lo:[1,1,0] neg_hi:[0,1,0]
	v_pk_fma_f32 v[38:39], v[76:77], v[48:49], v[92:93] op_sel_hi:[1,0,1]
	v_pk_fma_f32 v[42:43], v[76:77], v[48:49], v[92:93] op_sel_hi:[1,0,1] neg_lo:[0,0,1] neg_hi:[0,0,1]
	v_pk_fma_f32 v[48:49], v[82:83], v[56:57], v[94:95] op_sel_hi:[1,0,1] neg_lo:[0,0,1] neg_hi:[0,0,1]
	v_xor_b32_e32 v75, 0x80000000, v42
	v_mov_b32_e32 v74, v43
	v_pk_fma_f32 v[42:43], v[82:83], v[56:57], v[94:95] op_sel_hi:[1,0,1]
	v_pk_mul_f32 v[56:57], v[48:49], v[124:125] op_sel_hi:[1,0] neg_lo:[0,1] neg_hi:[0,1]
	v_xor_b32_e32 v76, 0x80000000, v49
	v_mov_b32_e32 v77, v48
	v_pk_fma_f32 v[48:49], v[84:85], v[58:59], v[106:107] op_sel_hi:[1,0,1]
	v_pk_fma_f32 v[58:59], v[84:85], v[58:59], v[106:107] op_sel_hi:[1,0,1] neg_lo:[0,0,1] neg_hi:[0,0,1]
	v_pk_fma_f32 v[56:57], v[76:77], v[118:119], v[56:57] op_sel_hi:[1,0,1] neg_lo:[0,1,0] neg_hi:[0,1,0]
	v_pk_mul_f32 v[76:77], v[58:59], v[34:35] op_sel_hi:[1,0] neg_lo:[0,1] neg_hi:[0,1]
	v_pk_fma_f32 v[58:59], v[58:59], v[30:31], v[76:77] op_sel:[1,0,0] op_sel_hi:[0,0,1] neg_lo:[1,1,0] neg_hi:[0,1,0]
	v_pk_fma_f32 v[76:77], v[86:87], v[60:61], v[108:109] op_sel_hi:[1,0,1]
	v_pk_fma_f32 v[60:61], v[86:87], v[60:61], v[108:109] op_sel_hi:[1,0,1] neg_lo:[0,0,1] neg_hi:[0,0,1]
	v_pk_mul_f32 v[82:83], v[60:61], v[122:123] op_sel_hi:[1,0] neg_lo:[0,1] neg_hi:[0,1]
	v_pk_fma_f32 v[60:61], v[60:61], v[120:121], v[82:83] op_sel:[1,0,0] op_sel_hi:[0,0,1] neg_lo:[1,1,0] neg_hi:[0,1,0]
	v_pk_fma_f32 v[82:83], v[80:81], v[62:63], v[110:111] op_sel_hi:[1,0,1]
	v_pk_fma_f32 v[62:63], v[80:81], v[62:63], v[110:111] op_sel_hi:[1,0,1] neg_lo:[0,0,1] neg_hi:[0,0,1]
	v_pk_add_f32 v[84:85], v[126:127], v[38:39] neg_lo:[0,1] neg_hi:[0,1]
	v_pk_mul_f32 v[80:81], v[62:63], v[10:11] op_sel:[1,0] op_sel_hi:[0,0] neg_lo:[1,1] neg_hi:[0,1]
	v_pk_fma_f32 v[62:63], v[62:63], v[10:11], v[80:81] op_sel_hi:[1,0,1] neg_lo:[0,1,0] neg_hi:[0,1,0]
	v_pk_fma_f32 v[80:81], v[78:79], v[50:51], v[112:113] op_sel_hi:[1,0,1]
	v_pk_fma_f32 v[50:51], v[78:79], v[50:51], v[112:113] op_sel_hi:[1,0,1] neg_lo:[0,0,1] neg_hi:[0,0,1]
	v_pk_mul_f32 v[78:79], v[50:51], v[122:123] op_sel:[1,0] op_sel_hi:[0,0] neg_lo:[1,1] neg_hi:[0,1]
	v_pk_fma_f32 v[50:51], v[50:51], v[120:121], v[78:79] op_sel_hi:[1,0,1] neg_lo:[0,1,0] neg_hi:[0,1,0]
	v_pk_fma_f32 v[78:79], v[70:71], v[24:25], v[114:115] op_sel_hi:[1,0,1]
	v_pk_fma_f32 v[24:25], v[70:71], v[24:25], v[114:115] op_sel_hi:[1,0,1] neg_lo:[0,0,1] neg_hi:[0,0,1]
	v_pk_mul_f32 v[70:71], v[24:25], v[34:35] op_sel:[1,0] op_sel_hi:[0,0] neg_lo:[1,1] neg_hi:[0,1]
	v_pk_fma_f32 v[70:71], v[24:25], v[30:31], v[70:71] op_sel_hi:[1,0,1] neg_lo:[0,1,0] neg_hi:[0,1,0]
	v_pk_fma_f32 v[24:25], v[72:73], v[44:45], v[116:117] op_sel_hi:[1,0,1]
	v_pk_fma_f32 v[44:45], v[72:73], v[44:45], v[116:117] op_sel_hi:[1,0,1] neg_lo:[0,0,1] neg_hi:[0,0,1]
	v_pk_mul_f32 v[72:73], v[44:45], v[124:125] op_sel:[1,0] op_sel_hi:[0,0] neg_lo:[1,1] neg_hi:[0,1]
	v_pk_fma_f32 v[72:73], v[118:119], v[44:45], v[72:73] op_sel_hi:[0,1,1] neg_lo:[1,0,0] neg_hi:[1,0,0]
	v_pk_add_f32 v[44:45], v[126:127], v[38:39]
	v_pk_add_f32 v[38:39], v[16:17], v[42:43]
	v_pk_add_f32 v[16:17], v[16:17], v[42:43] neg_lo:[0,1] neg_hi:[0,1]
	v_pk_mul_f32 v[42:43], v[16:17], v[34:35] op_sel:[1,0] op_sel_hi:[0,0] neg_lo:[1,1] neg_hi:[0,1]
	v_pk_fma_f32 v[42:43], v[16:17], v[30:31], v[42:43] op_sel_hi:[1,0,1]
	v_pk_add_f32 v[16:17], v[18:19], v[48:49]
	v_pk_add_f32 v[18:19], v[18:19], v[48:49] neg_lo:[0,1] neg_hi:[0,1]
	v_pk_mul_f32 v[48:49], v[18:19], v[10:11] op_sel:[1,0] op_sel_hi:[0,0] neg_lo:[1,1] neg_hi:[0,1]
	v_pk_fma_f32 v[18:19], v[18:19], v[10:11], v[48:49] op_sel_hi:[1,0,1]
	v_pk_add_f32 v[48:49], v[20:21], v[76:77]
	v_pk_add_f32 v[20:21], v[20:21], v[76:77] neg_lo:[0,1] neg_hi:[0,1]
	v_pk_mul_f32 v[76:77], v[20:21], v[34:35] op_sel_hi:[1,0]
	v_xor_b32_e32 v86, 0x80000000, v21
	v_mov_b32_e32 v87, v20
	v_pk_add_f32 v[20:21], v[22:23], v[82:83]
	v_pk_add_f32 v[22:23], v[22:23], v[82:83] neg_lo:[0,1] neg_hi:[0,1]
	v_pk_fma_f32 v[76:77], v[86:87], v[30:31], v[76:77] op_sel_hi:[1,0,1] neg_lo:[0,1,0] neg_hi:[0,1,0]
	v_xor_b32_e32 v83, 0x80000000, v22
	v_mov_b32_e32 v82, v23
	v_pk_add_f32 v[22:23], v[26:27], v[80:81]
	v_pk_add_f32 v[26:27], v[26:27], v[80:81] neg_lo:[0,1] neg_hi:[0,1]
	v_pk_mul_f32 v[80:81], v[26:27], v[34:35] op_sel_hi:[1,0] neg_lo:[0,1] neg_hi:[0,1]
	v_pk_fma_f32 v[26:27], v[30:31], v[26:27], v[80:81] op_sel:[0,1,0] op_sel_hi:[0,0,1] neg_lo:[1,1,0] neg_hi:[1,0,0]
	v_pk_add_f32 v[80:81], v[28:29], v[78:79]
	v_pk_add_f32 v[28:29], v[28:29], v[78:79] neg_lo:[0,1] neg_hi:[0,1]
	v_pk_add_f32 v[86:87], v[44:45], v[20:21] neg_lo:[0,1] neg_hi:[0,1]
	v_pk_mul_f32 v[78:79], v[10:11], v[28:29] op_sel:[0,1] op_sel_hi:[0,0] neg_lo:[1,1] neg_hi:[1,0]
	v_pk_fma_f32 v[78:79], v[28:29], v[10:11], v[78:79] op_sel_hi:[1,0,1] neg_lo:[0,1,0] neg_hi:[0,1,0]
	v_pk_add_f32 v[28:29], v[32:33], v[24:25]
	v_pk_add_f32 v[24:25], v[32:33], v[24:25] neg_lo:[0,1] neg_hi:[0,1]
	v_pk_mul_f32 v[32:33], v[34:35], v[24:25] op_sel:[0,1] op_sel_hi:[0,0] neg_lo:[1,1] neg_hi:[1,0]
	v_pk_fma_f32 v[32:33], v[30:31], v[24:25], v[32:33] op_sel_hi:[0,1,1] neg_lo:[1,0,0] neg_hi:[1,0,0]
	v_pk_add_f32 v[24:25], v[44:45], v[20:21]
	v_pk_add_f32 v[20:21], v[38:39], v[22:23]
	v_pk_add_f32 v[22:23], v[38:39], v[22:23] neg_lo:[0,1] neg_hi:[0,1]
	v_pk_mul_f32 v[38:39], v[10:11], v[22:23] op_sel:[0,1] op_sel_hi:[0,0] neg_lo:[1,1] neg_hi:[1,0]
	v_pk_fma_f32 v[22:23], v[22:23], v[10:11], v[38:39] op_sel_hi:[1,0,1]
	v_pk_add_f32 v[38:39], v[16:17], v[80:81]
	v_pk_add_f32 v[16:17], v[16:17], v[80:81] neg_lo:[0,1] neg_hi:[0,1]
	v_xor_b32_e32 v81, 0x80000000, v16
	v_mov_b32_e32 v80, v17
	v_pk_add_f32 v[16:17], v[48:49], v[28:29]
	v_pk_add_f32 v[28:29], v[48:49], v[28:29] neg_lo:[0,1] neg_hi:[0,1]
	v_pk_mul_f32 v[44:45], v[10:11], v[28:29] op_sel:[0,1] op_sel_hi:[0,0] neg_lo:[1,1] neg_hi:[1,0]
	v_pk_fma_f32 v[48:49], v[10:11], v[28:29], v[44:45] op_sel_hi:[0,1,1] neg_lo:[1,0,0] neg_hi:[1,0,0]
	v_pk_add_f32 v[28:29], v[24:25], v[38:39]
	v_pk_add_f32 v[24:25], v[24:25], v[38:39] neg_lo:[0,1] neg_hi:[0,1]
	v_pk_add_f32 v[38:39], v[20:21], v[16:17]
	v_pk_add_f32 v[16:17], v[20:21], v[16:17] neg_lo:[0,1] neg_hi:[0,1]
	v_pk_add_f32 v[88:89], v[28:29], v[38:39]
	v_pk_add_f32 v[44:45], v[24:25], v[16:17] op_sel:[0,1] op_sel_hi:[1,0] neg_hi:[0,1]
	v_pk_add_f32 v[20:21], v[24:25], v[16:17] op_sel:[0,1] op_sel_hi:[1,0] neg_lo:[0,1]
	v_pk_add_f32 v[24:25], v[22:23], v[48:49]
	v_pk_add_f32 v[22:23], v[22:23], v[48:49] neg_lo:[0,1] neg_hi:[0,1]
	v_pk_add_f32 v[16:17], v[86:87], v[80:81]
	v_pk_add_f32 v[80:81], v[86:87], v[80:81] neg_lo:[0,1] neg_hi:[0,1]
	v_pk_add_f32 v[28:29], v[28:29], v[38:39] neg_lo:[0,1] neg_hi:[0,1]
	v_pk_add_f32 v[86:87], v[16:17], v[24:25]
	v_pk_add_f32 v[24:25], v[16:17], v[24:25] neg_lo:[0,1] neg_hi:[0,1]
	v_pk_add_f32 v[38:39], v[80:81], v[22:23] op_sel:[0,1] op_sel_hi:[1,0] neg_hi:[0,1]
	v_pk_add_f32 v[16:17], v[80:81], v[22:23] op_sel:[0,1] op_sel_hi:[1,0] neg_lo:[0,1]
	v_pk_add_f32 v[48:49], v[42:43], v[26:27]
	v_pk_add_f32 v[26:27], v[42:43], v[26:27] neg_lo:[0,1] neg_hi:[0,1]
	v_pk_add_f32 v[22:23], v[84:85], v[82:83]
	v_pk_mul_f32 v[42:43], v[10:11], v[26:27] op_sel:[0,1] op_sel_hi:[0,0] neg_lo:[1,1] neg_hi:[1,0]
	v_pk_fma_f32 v[26:27], v[10:11], v[26:27], v[42:43] op_sel_hi:[0,1,1]
	v_pk_add_f32 v[42:43], v[18:19], v[78:79]
	v_pk_add_f32 v[18:19], v[18:19], v[78:79] neg_lo:[0,1] neg_hi:[0,1]
	v_pk_add_f32 v[80:81], v[84:85], v[82:83] neg_lo:[0,1] neg_hi:[0,1]
	v_xor_b32_e32 v79, 0x80000000, v18
	v_mov_b32_e32 v78, v19
	v_pk_add_f32 v[18:19], v[76:77], v[32:33]
	v_pk_add_f32 v[32:33], v[76:77], v[32:33] neg_lo:[0,1] neg_hi:[0,1]
	v_pk_mul_f32 v[76:77], v[10:11], v[32:33] op_sel:[0,1] op_sel_hi:[0,0] neg_lo:[1,1] neg_hi:[1,0]
	v_pk_fma_f32 v[76:77], v[10:11], v[32:33], v[76:77] op_sel_hi:[0,1,1] neg_lo:[1,0,0] neg_hi:[1,0,0]
	v_pk_add_f32 v[32:33], v[22:23], v[42:43]
	v_pk_add_f32 v[22:23], v[22:23], v[42:43] neg_lo:[0,1] neg_hi:[0,1]
	v_pk_add_f32 v[42:43], v[48:49], v[18:19]
	v_pk_add_f32 v[18:19], v[48:49], v[18:19] neg_lo:[0,1] neg_hi:[0,1]
	v_pk_add_f32 v[84:85], v[32:33], v[42:43]
	v_pk_add_f32 v[32:33], v[32:33], v[42:43] neg_lo:[0,1] neg_hi:[0,1]
	v_pk_add_f32 v[42:43], v[26:27], v[76:77]
	v_pk_add_f32 v[26:27], v[26:27], v[76:77] neg_lo:[0,1] neg_hi:[0,1]
	v_xor_b32_e32 v83, 0x80000000, v18
	v_mov_b32_e32 v82, v19
	v_pk_add_f32 v[18:19], v[80:81], v[78:79]
	v_pk_add_f32 v[78:79], v[80:81], v[78:79] neg_lo:[0,1] neg_hi:[0,1]
	v_xor_b32_e32 v77, 0x80000000, v26
	v_mov_b32_e32 v76, v27
	v_pk_add_f32 v[80:81], v[18:19], v[42:43]
	v_pk_add_f32 v[26:27], v[18:19], v[42:43] neg_lo:[0,1] neg_hi:[0,1]
	v_pk_add_f32 v[42:43], v[78:79], v[76:77]
	v_pk_add_f32 v[18:19], v[78:79], v[76:77] neg_lo:[0,1] neg_hi:[0,1]
	v_pk_add_f32 v[76:77], v[36:37], v[74:75]
	v_pk_add_f32 v[74:75], v[36:37], v[74:75] neg_lo:[0,1] neg_hi:[0,1]
	v_pk_add_f32 v[36:37], v[40:41], v[56:57]
	v_pk_add_f32 v[40:41], v[40:41], v[56:57] neg_lo:[0,1] neg_hi:[0,1]
	v_pk_add_f32 v[48:49], v[22:23], v[82:83]
	v_pk_mul_f32 v[56:57], v[34:35], v[40:41] op_sel:[0,1] op_sel_hi:[0,0] neg_lo:[1,1] neg_hi:[1,0]
	v_pk_fma_f32 v[40:41], v[30:31], v[40:41], v[56:57] op_sel_hi:[0,1,1]
	v_pk_add_f32 v[56:57], v[46:47], v[58:59]
	v_pk_add_f32 v[46:47], v[46:47], v[58:59] neg_lo:[0,1] neg_hi:[0,1]
	v_pk_add_f32 v[22:23], v[22:23], v[82:83] neg_lo:[0,1] neg_hi:[0,1]
	v_pk_mul_f32 v[58:59], v[10:11], v[46:47] op_sel:[0,1] op_sel_hi:[0,0] neg_lo:[1,1] neg_hi:[1,0]
	v_pk_fma_f32 v[58:59], v[10:11], v[46:47], v[58:59] op_sel_hi:[0,1,1]
	v_pk_add_f32 v[46:47], v[52:53], v[60:61]
	v_pk_add_f32 v[52:53], v[52:53], v[60:61] neg_lo:[0,1] neg_hi:[0,1]
	v_pk_mul_f32 v[60:61], v[30:31], v[52:53] op_sel:[0,1] op_sel_hi:[0,0] neg_lo:[1,1] neg_hi:[1,0]
	v_pk_fma_f32 v[60:61], v[34:35], v[52:53], v[60:61] op_sel_hi:[0,1,1]
	v_pk_add_f32 v[52:53], v[54:55], v[62:63]
	v_pk_add_f32 v[54:55], v[54:55], v[62:63] neg_lo:[0,1] neg_hi:[0,1]
	v_xor_b32_e32 v63, 0x80000000, v54
	v_mov_b32_e32 v62, v55
	v_pk_add_f32 v[54:55], v[64:65], v[50:51]
	v_pk_add_f32 v[50:51], v[64:65], v[50:51] neg_lo:[0,1] neg_hi:[0,1]
	v_pk_mul_f32 v[64:65], v[30:31], v[50:51] op_sel:[0,1] op_sel_hi:[0,0] neg_lo:[1,1] neg_hi:[1,0]
	v_pk_fma_f32 v[50:51], v[34:35], v[50:51], v[64:65] op_sel_hi:[0,1,1] neg_lo:[1,0,0] neg_hi:[1,0,0]
	v_pk_add_f32 v[64:65], v[66:67], v[70:71]
	v_pk_add_f32 v[66:67], v[66:67], v[70:71] neg_lo:[0,1] neg_hi:[0,1]
	v_pk_mul_f32 v[70:71], v[10:11], v[66:67] op_sel:[0,1] op_sel_hi:[0,0] neg_lo:[1,1] neg_hi:[1,0]
	v_pk_fma_f32 v[66:67], v[10:11], v[66:67], v[70:71] op_sel_hi:[0,1,1] neg_lo:[1,0,0] neg_hi:[1,0,0]
	v_pk_add_f32 v[70:71], v[68:69], v[72:73]
	v_pk_add_f32 v[68:69], v[68:69], v[72:73] neg_lo:[0,1] neg_hi:[0,1]
	v_pk_mul_f32 v[34:35], v[34:35], v[68:69] op_sel:[0,1] op_sel_hi:[0,0] neg_lo:[1,1] neg_hi:[1,0]
	v_pk_fma_f32 v[34:35], v[30:31], v[68:69], v[34:35] op_sel_hi:[0,1,1] neg_lo:[1,0,0] neg_hi:[1,0,0]
	v_pk_add_f32 v[30:31], v[76:77], v[52:53]
	v_pk_add_f32 v[68:69], v[76:77], v[52:53] neg_lo:[0,1] neg_hi:[0,1]
	v_pk_add_f32 v[52:53], v[54:55], v[36:37]
	v_pk_add_f32 v[36:37], v[36:37], v[54:55] neg_lo:[0,1] neg_hi:[0,1]
	v_pk_mul_f32 v[54:55], v[10:11], v[36:37] op_sel:[0,1] op_sel_hi:[0,0] neg_lo:[1,1] neg_hi:[1,0]
	v_pk_fma_f32 v[54:55], v[10:11], v[36:37], v[54:55] op_sel_hi:[0,1,1]
	v_pk_add_f32 v[36:37], v[56:57], v[64:65]
	v_pk_add_f32 v[56:57], v[56:57], v[64:65] neg_lo:[0,1] neg_hi:[0,1]
	v_xor_b32_e32 v65, 0x80000000, v56
	v_mov_b32_e32 v64, v57
	v_pk_add_f32 v[56:57], v[46:47], v[70:71]
	v_pk_add_f32 v[46:47], v[46:47], v[70:71] neg_lo:[0,1] neg_hi:[0,1]
	v_pk_mul_f32 v[70:71], v[10:11], v[46:47] op_sel:[0,1] op_sel_hi:[0,0] neg_lo:[1,1] neg_hi:[1,0]
	v_pk_fma_f32 v[46:47], v[10:11], v[46:47], v[70:71] op_sel_hi:[0,1,1] neg_lo:[1,0,0] neg_hi:[1,0,0]
	v_pk_add_f32 v[70:71], v[30:31], v[36:37]
	v_pk_add_f32 v[30:31], v[30:31], v[36:37] neg_lo:[0,1] neg_hi:[0,1]
	v_pk_add_f32 v[36:37], v[52:53], v[56:57]
	v_pk_add_f32 v[52:53], v[52:53], v[56:57] neg_lo:[0,1] neg_hi:[0,1]
	v_pk_add_f32 v[72:73], v[70:71], v[36:37]
	v_xor_b32_e32 v57, 0x80000000, v52
	v_mov_b32_e32 v56, v53
	v_pk_add_f32 v[52:53], v[70:71], v[36:37] neg_lo:[0,1] neg_hi:[0,1]
	v_pk_add_f32 v[70:71], v[30:31], v[56:57]
	v_pk_add_f32 v[36:37], v[30:31], v[56:57] neg_lo:[0,1] neg_hi:[0,1]
	v_pk_add_f32 v[30:31], v[68:69], v[64:65]
	v_pk_add_f32 v[56:57], v[68:69], v[64:65] neg_lo:[0,1] neg_hi:[0,1]
	v_pk_add_f32 v[64:65], v[54:55], v[46:47]
	v_pk_add_f32 v[46:47], v[54:55], v[46:47] neg_lo:[0,1] neg_hi:[0,1]
	v_pk_add_f32 v[68:69], v[30:31], v[64:65]
	v_xor_b32_e32 v55, 0x80000000, v46
	v_mov_b32_e32 v54, v47
	v_pk_add_f32 v[46:47], v[30:31], v[64:65] neg_lo:[0,1] neg_hi:[0,1]
	v_pk_add_f32 v[64:65], v[56:57], v[54:55]
	v_pk_add_f32 v[30:31], v[56:57], v[54:55] neg_lo:[0,1] neg_hi:[0,1]
	v_pk_add_f32 v[54:55], v[74:75], v[62:63]
	v_pk_add_f32 v[56:57], v[74:75], v[62:63] neg_lo:[0,1] neg_hi:[0,1]
	v_pk_add_f32 v[62:63], v[50:51], v[40:41]
	v_pk_add_f32 v[40:41], v[40:41], v[50:51] neg_lo:[0,1] neg_hi:[0,1]
	v_pk_mul_f32 v[50:51], v[10:11], v[40:41] op_sel:[0,1] op_sel_hi:[0,0] neg_lo:[1,1] neg_hi:[1,0]
	v_pk_fma_f32 v[50:51], v[10:11], v[40:41], v[50:51] op_sel_hi:[0,1,1]
	v_pk_add_f32 v[40:41], v[58:59], v[66:67]
	v_pk_add_f32 v[58:59], v[58:59], v[66:67] neg_lo:[0,1] neg_hi:[0,1]
	v_xor_b32_e32 v67, 0x80000000, v58
	v_mov_b32_e32 v66, v59
	v_pk_add_f32 v[58:59], v[60:61], v[34:35]
	v_pk_add_f32 v[34:35], v[60:61], v[34:35] neg_lo:[0,1] neg_hi:[0,1]
	v_pk_mul_f32 v[60:61], v[10:11], v[34:35] op_sel:[0,1] op_sel_hi:[0,0] neg_lo:[1,1] neg_hi:[1,0]
	v_pk_fma_f32 v[34:35], v[10:11], v[34:35], v[60:61] op_sel_hi:[0,1,1] neg_lo:[1,0,0] neg_hi:[1,0,0]
	v_pk_add_f32 v[60:61], v[54:55], v[40:41]
	v_pk_add_f32 v[40:41], v[54:55], v[40:41] neg_lo:[0,1] neg_hi:[0,1]
	v_pk_add_f32 v[54:55], v[62:63], v[58:59]
	v_pk_add_f32 v[58:59], v[62:63], v[58:59] neg_lo:[0,1] neg_hi:[0,1]
	v_lshl_add_u32 v10, v13, 3, 0
	v_xor_b32_e32 v63, 0x80000000, v58
	v_mov_b32_e32 v62, v59
	v_pk_add_f32 v[58:59], v[60:61], v[54:55]
	v_pk_add_f32 v[54:55], v[60:61], v[54:55] neg_lo:[0,1] neg_hi:[0,1]
	v_pk_add_f32 v[60:61], v[40:41], v[62:63]
	v_pk_add_f32 v[40:41], v[40:41], v[62:63] neg_lo:[0,1] neg_hi:[0,1]
	v_pk_add_f32 v[62:63], v[56:57], v[66:67]
	v_pk_add_f32 v[56:57], v[56:57], v[66:67] neg_lo:[0,1] neg_hi:[0,1]
	v_pk_add_f32 v[66:67], v[50:51], v[34:35]
	v_pk_add_f32 v[34:35], v[50:51], v[34:35] neg_lo:[0,1] neg_hi:[0,1]
	v_pk_add_f32 v[76:77], v[62:63], v[66:67]
	v_pk_add_f32 v[50:51], v[62:63], v[66:67] neg_lo:[0,1] neg_hi:[0,1]
	v_pk_add_f32 v[62:63], v[56:57], v[34:35] op_sel:[0,1] op_sel_hi:[1,0] neg_hi:[0,1]
	v_pk_add_f32 v[34:35], v[56:57], v[34:35] op_sel:[0,1] op_sel_hi:[1,0] neg_lo:[0,1]
	v_pk_mul_f32 v[56:57], v[88:89], s[14:15] op_sel:[1,0] neg_lo:[1,0]
	v_pk_fma_f32 v[56:57], v[88:89], s[42:43], v[56:57] op_sel_hi:[0,1,1]
	ds_write_b64 v10, v[56:57]
	v_pk_fma_f32 v[56:57], v[180:181], s[92:93], v[180:181] op_sel:[1,0,0] op_sel_hi:[0,1,1]
	v_pk_mul_f32 v[66:67], v[56:57], v[72:73] op_sel:[1,1] op_sel_hi:[0,1] neg_lo:[0,1]
	v_pk_fma_f32 v[66:67], v[56:57], v[72:73], v[66:67] op_sel_hi:[1,0,1]
	ds_write_b64 v10, v[66:67] offset:4224
	v_pk_mul_f32 v[66:67], v[180:181], v[56:57] op_sel:[1,1] op_sel_hi:[0,1] neg_lo:[0,1]
	v_pk_fma_f32 v[56:57], v[180:181], v[56:57], v[66:67] op_sel_hi:[1,0,1]
	v_pk_mul_f32 v[66:67], v[56:57], v[84:85] op_sel:[1,1] op_sel_hi:[0,1] neg_lo:[0,1]
	v_pk_fma_f32 v[66:67], v[56:57], v[84:85], v[66:67] op_sel_hi:[1,0,1]
	ds_write_b64 v10, v[66:67] offset:8448
	v_pk_mul_f32 v[66:67], v[180:181], v[56:57] op_sel:[1,1] op_sel_hi:[0,1] neg_lo:[0,1]
	v_pk_fma_f32 v[56:57], v[180:181], v[56:57], v[66:67] op_sel_hi:[1,0,1]
	v_pk_mul_f32 v[66:67], v[56:57], v[58:59] op_sel:[1,1] op_sel_hi:[0,1] neg_lo:[0,1]
	v_pk_fma_f32 v[58:59], v[56:57], v[58:59], v[66:67] op_sel_hi:[1,0,1]
	ds_write_b64 v10, v[58:59] offset:12672
	v_pk_mul_f32 v[58:59], v[180:181], v[56:57] op_sel:[1,1] op_sel_hi:[0,1] neg_lo:[0,1]
	v_pk_fma_f32 v[56:57], v[180:181], v[56:57], v[58:59] op_sel_hi:[1,0,1]
	v_pk_mul_f32 v[58:59], v[56:57], v[86:87] op_sel:[1,1] op_sel_hi:[0,1] neg_lo:[0,1]
	v_pk_fma_f32 v[58:59], v[56:57], v[86:87], v[58:59] op_sel_hi:[1,0,1]
	ds_write_b64 v10, v[58:59] offset:16896
	v_pk_mul_f32 v[58:59], v[180:181], v[56:57] op_sel:[1,1] op_sel_hi:[0,1] neg_lo:[0,1]
	v_pk_fma_f32 v[56:57], v[180:181], v[56:57], v[58:59] op_sel_hi:[1,0,1]
	v_pk_mul_f32 v[58:59], v[56:57], v[68:69] op_sel:[1,1] op_sel_hi:[0,1] neg_lo:[0,1]
	v_pk_fma_f32 v[58:59], v[56:57], v[68:69], v[58:59] op_sel_hi:[1,0,1]
	ds_write_b64 v10, v[58:59] offset:21120
	v_pk_mul_f32 v[58:59], v[180:181], v[56:57] op_sel:[1,1] op_sel_hi:[0,1] neg_lo:[0,1]
	v_pk_fma_f32 v[56:57], v[180:181], v[56:57], v[58:59] op_sel_hi:[1,0,1]
	v_pk_mul_f32 v[58:59], v[80:81], v[56:57] op_sel:[1,1] op_sel_hi:[1,0] neg_lo:[1,0]
	v_pk_fma_f32 v[58:59], v[80:81], v[56:57], v[58:59] op_sel_hi:[0,1,1]
	ds_write_b64 v10, v[58:59] offset:25344
	v_pk_mul_f32 v[58:59], v[180:181], v[56:57] op_sel:[1,1] op_sel_hi:[0,1] neg_lo:[0,1]
	v_pk_fma_f32 v[56:57], v[180:181], v[56:57], v[58:59] op_sel_hi:[1,0,1]
	v_pk_mul_f32 v[58:59], v[76:77], v[56:57] op_sel:[1,1] op_sel_hi:[1,0] neg_lo:[1,0]
	v_pk_fma_f32 v[58:59], v[76:77], v[56:57], v[58:59] op_sel_hi:[0,1,1]
	ds_write_b64 v10, v[58:59] offset:29568
	v_pk_mul_f32 v[58:59], v[180:181], v[56:57] op_sel:[1,1] op_sel_hi:[0,1] neg_lo:[0,1]
	v_pk_fma_f32 v[56:57], v[180:181], v[56:57], v[58:59] op_sel_hi:[1,0,1]
	v_pk_mul_f32 v[58:59], v[44:45], v[56:57] op_sel:[1,1] op_sel_hi:[1,0] neg_lo:[1,0]
	v_pk_fma_f32 v[44:45], v[44:45], v[56:57], v[58:59] op_sel_hi:[0,1,1]
	ds_write_b64 v10, v[44:45] offset:33792
	v_pk_mul_f32 v[44:45], v[180:181], v[56:57] op_sel:[1,1] op_sel_hi:[0,1] neg_lo:[0,1]
	v_pk_fma_f32 v[44:45], v[180:181], v[56:57], v[44:45] op_sel_hi:[1,0,1]
	v_pk_mul_f32 v[56:57], v[70:71], v[44:45] op_sel:[1,1] op_sel_hi:[1,0] neg_lo:[1,0]
	v_pk_fma_f32 v[56:57], v[70:71], v[44:45], v[56:57] op_sel_hi:[0,1,1]
	ds_write_b64 v10, v[56:57] offset:38016
	v_pk_mul_f32 v[56:57], v[180:181], v[44:45] op_sel:[1,1] op_sel_hi:[0,1] neg_lo:[0,1]
	v_pk_fma_f32 v[44:45], v[180:181], v[44:45], v[56:57] op_sel_hi:[1,0,1]
	v_pk_mul_f32 v[56:57], v[48:49], v[44:45] op_sel:[1,1] op_sel_hi:[1,0] neg_lo:[1,0]
	v_pk_fma_f32 v[48:49], v[48:49], v[44:45], v[56:57] op_sel_hi:[0,1,1]
	ds_write_b64 v10, v[48:49] offset:42240
	v_pk_mul_f32 v[48:49], v[180:181], v[44:45] op_sel:[1,1] op_sel_hi:[0,1] neg_lo:[0,1]
	v_pk_fma_f32 v[44:45], v[180:181], v[44:45], v[48:49] op_sel_hi:[1,0,1]
	v_pk_mul_f32 v[48:49], v[60:61], v[44:45] op_sel:[1,1] op_sel_hi:[1,0] neg_lo:[1,0]
	v_pk_fma_f32 v[48:49], v[60:61], v[44:45], v[48:49] op_sel_hi:[0,1,1]
	ds_write_b64 v10, v[48:49] offset:46464
	v_pk_mul_f32 v[48:49], v[180:181], v[44:45] op_sel:[1,1] op_sel_hi:[0,1] neg_lo:[0,1]
	v_pk_fma_f32 v[44:45], v[180:181], v[44:45], v[48:49] op_sel_hi:[1,0,1]
	v_pk_mul_f32 v[48:49], v[38:39], v[44:45] op_sel:[1,1] op_sel_hi:[1,0] neg_lo:[1,0]
	v_pk_fma_f32 v[38:39], v[38:39], v[44:45], v[48:49] op_sel_hi:[0,1,1]
	ds_write_b64 v10, v[38:39] offset:50688
	v_pk_mul_f32 v[38:39], v[180:181], v[44:45] op_sel:[1,1] op_sel_hi:[0,1] neg_lo:[0,1]
	v_pk_fma_f32 v[38:39], v[180:181], v[44:45], v[38:39] op_sel_hi:[1,0,1]
	v_pk_mul_f32 v[44:45], v[64:65], v[38:39] op_sel:[1,1] op_sel_hi:[1,0] neg_lo:[1,0]
	v_pk_fma_f32 v[44:45], v[64:65], v[38:39], v[44:45] op_sel_hi:[0,1,1]
	ds_write_b64 v10, v[44:45] offset:54912
	v_pk_mul_f32 v[44:45], v[180:181], v[38:39] op_sel:[1,1] op_sel_hi:[0,1] neg_lo:[0,1]
	v_pk_fma_f32 v[38:39], v[180:181], v[38:39], v[44:45] op_sel_hi:[1,0,1]
	v_pk_mul_f32 v[44:45], v[42:43], v[38:39] op_sel:[1,1] op_sel_hi:[1,0] neg_lo:[1,0]
	v_pk_fma_f32 v[42:43], v[42:43], v[38:39], v[44:45] op_sel_hi:[0,1,1]
	ds_write_b64 v10, v[42:43] offset:59136
	v_pk_mul_f32 v[42:43], v[180:181], v[38:39] op_sel:[1,1] op_sel_hi:[0,1] neg_lo:[0,1]
	v_pk_fma_f32 v[38:39], v[180:181], v[38:39], v[42:43] op_sel_hi:[1,0,1]
	v_pk_mul_f32 v[42:43], v[62:63], v[38:39] op_sel:[1,1] op_sel_hi:[1,0] neg_lo:[1,0]
	v_pk_fma_f32 v[42:43], v[62:63], v[38:39], v[42:43] op_sel_hi:[0,1,1]
	ds_write_b64 v10, v[42:43] offset:63360
	v_pk_mul_f32 v[42:43], v[180:181], v[38:39] op_sel:[1,1] op_sel_hi:[0,1] neg_lo:[0,1]
	v_pk_fma_f32 v[38:39], v[180:181], v[38:39], v[42:43] op_sel_hi:[1,0,1]
	v_pk_mul_f32 v[42:43], v[28:29], v[38:39] op_sel:[1,1] op_sel_hi:[1,0] neg_lo:[1,0]
	v_add_u32_e32 v13, 0x10800, v10
	v_pk_fma_f32 v[28:29], v[28:29], v[38:39], v[42:43] op_sel_hi:[0,1,1]
	ds_write_b64 v13, v[28:29]
	v_pk_mul_f32 v[28:29], v[180:181], v[38:39] op_sel:[1,1] op_sel_hi:[0,1] neg_lo:[0,1]
	v_pk_fma_f32 v[28:29], v[180:181], v[38:39], v[28:29] op_sel_hi:[1,0,1]
	v_pk_mul_f32 v[38:39], v[52:53], v[28:29] op_sel:[1,1] op_sel_hi:[1,0] neg_lo:[1,0]
	v_add_u32_e32 v13, 0x11880, v10
	v_pk_fma_f32 v[38:39], v[52:53], v[28:29], v[38:39] op_sel_hi:[0,1,1]
	ds_write_b64 v13, v[38:39]
	v_pk_mul_f32 v[38:39], v[180:181], v[28:29] op_sel:[1,1] op_sel_hi:[0,1] neg_lo:[0,1]
	v_pk_fma_f32 v[28:29], v[180:181], v[28:29], v[38:39] op_sel_hi:[1,0,1]
	v_pk_mul_f32 v[38:39], v[32:33], v[28:29] op_sel:[1,1] op_sel_hi:[1,0] neg_lo:[1,0]
	v_add_u32_e32 v13, 0x12900, v10
	v_pk_fma_f32 v[32:33], v[32:33], v[28:29], v[38:39] op_sel_hi:[0,1,1]
	ds_write_b64 v13, v[32:33]
	v_pk_mul_f32 v[32:33], v[180:181], v[28:29] op_sel:[1,1] op_sel_hi:[0,1] neg_lo:[0,1]
	v_pk_fma_f32 v[28:29], v[180:181], v[28:29], v[32:33] op_sel_hi:[1,0,1]
	v_pk_mul_f32 v[32:33], v[54:55], v[28:29] op_sel:[1,1] op_sel_hi:[1,0] neg_lo:[1,0]
	v_add_u32_e32 v13, 0x13980, v10
	v_pk_fma_f32 v[32:33], v[54:55], v[28:29], v[32:33] op_sel_hi:[0,1,1]
	ds_write_b64 v13, v[32:33]
	v_pk_mul_f32 v[32:33], v[180:181], v[28:29] op_sel:[1,1] op_sel_hi:[0,1] neg_lo:[0,1]
	v_pk_fma_f32 v[28:29], v[180:181], v[28:29], v[32:33] op_sel_hi:[1,0,1]
	v_pk_mul_f32 v[32:33], v[24:25], v[28:29] op_sel:[1,1] op_sel_hi:[1,0] neg_lo:[1,0]
	v_add_u32_e32 v13, 0x14a00, v10
	v_pk_fma_f32 v[24:25], v[24:25], v[28:29], v[32:33] op_sel_hi:[0,1,1]
	ds_write_b64 v13, v[24:25]
	v_pk_mul_f32 v[24:25], v[180:181], v[28:29] op_sel:[1,1] op_sel_hi:[0,1] neg_lo:[0,1]
	v_pk_fma_f32 v[24:25], v[180:181], v[28:29], v[24:25] op_sel_hi:[1,0,1]
	v_pk_mul_f32 v[28:29], v[46:47], v[24:25] op_sel:[1,1] op_sel_hi:[1,0] neg_lo:[1,0]
	v_add_u32_e32 v13, 0x15a80, v10
	v_pk_fma_f32 v[28:29], v[46:47], v[24:25], v[28:29] op_sel_hi:[0,1,1]
	ds_write_b64 v13, v[28:29]
	v_pk_mul_f32 v[28:29], v[180:181], v[24:25] op_sel:[1,1] op_sel_hi:[0,1] neg_lo:[0,1]
	v_pk_fma_f32 v[24:25], v[180:181], v[24:25], v[28:29] op_sel_hi:[1,0,1]
	v_pk_mul_f32 v[28:29], v[26:27], v[24:25] op_sel:[1,1] op_sel_hi:[1,0] neg_lo:[1,0]
	v_add_u32_e32 v13, 0x16b00, v10
	v_pk_fma_f32 v[26:27], v[26:27], v[24:25], v[28:29] op_sel_hi:[0,1,1]
	ds_write_b64 v13, v[26:27]
	v_pk_mul_f32 v[26:27], v[180:181], v[24:25] op_sel:[1,1] op_sel_hi:[0,1] neg_lo:[0,1]
	v_pk_fma_f32 v[24:25], v[180:181], v[24:25], v[26:27] op_sel_hi:[1,0,1]
	v_pk_mul_f32 v[26:27], v[50:51], v[24:25] op_sel:[1,1] op_sel_hi:[1,0] neg_lo:[1,0]
	v_add_u32_e32 v13, 0x17b80, v10
	v_pk_fma_f32 v[26:27], v[50:51], v[24:25], v[26:27] op_sel_hi:[0,1,1]
	ds_write_b64 v13, v[26:27]
	v_pk_mul_f32 v[26:27], v[180:181], v[24:25] op_sel:[1,1] op_sel_hi:[0,1] neg_lo:[0,1]
	v_pk_fma_f32 v[24:25], v[180:181], v[24:25], v[26:27] op_sel_hi:[1,0,1]
	v_pk_mul_f32 v[26:27], v[20:21], v[24:25] op_sel:[1,1] op_sel_hi:[1,0] neg_lo:[1,0]
	v_add_u32_e32 v13, 0x18c00, v10
	v_pk_fma_f32 v[20:21], v[20:21], v[24:25], v[26:27] op_sel_hi:[0,1,1]
	ds_write_b64 v13, v[20:21]
	v_pk_mul_f32 v[20:21], v[180:181], v[24:25] op_sel:[1,1] op_sel_hi:[0,1] neg_lo:[0,1]
	v_pk_fma_f32 v[20:21], v[180:181], v[24:25], v[20:21] op_sel_hi:[1,0,1]
	v_pk_mul_f32 v[24:25], v[36:37], v[20:21] op_sel:[1,1] op_sel_hi:[1,0] neg_lo:[1,0]
	v_add_u32_e32 v13, 0x19c80, v10
	v_pk_fma_f32 v[24:25], v[36:37], v[20:21], v[24:25] op_sel_hi:[0,1,1]
	ds_write_b64 v13, v[24:25]
	v_pk_mul_f32 v[24:25], v[180:181], v[20:21] op_sel:[1,1] op_sel_hi:[0,1] neg_lo:[0,1]
	v_pk_fma_f32 v[20:21], v[180:181], v[20:21], v[24:25] op_sel_hi:[1,0,1]
	v_pk_mul_f32 v[24:25], v[22:23], v[20:21] op_sel:[1,1] op_sel_hi:[1,0] neg_lo:[1,0]
	v_add_u32_e32 v13, 0x1ad00, v10
	v_pk_fma_f32 v[22:23], v[22:23], v[20:21], v[24:25] op_sel_hi:[0,1,1]
	ds_write_b64 v13, v[22:23]
	v_pk_mul_f32 v[22:23], v[180:181], v[20:21] op_sel:[1,1] op_sel_hi:[0,1] neg_lo:[0,1]
	v_pk_fma_f32 v[20:21], v[180:181], v[20:21], v[22:23] op_sel_hi:[1,0,1]
	v_pk_mul_f32 v[22:23], v[40:41], v[20:21] op_sel:[1,1] op_sel_hi:[1,0] neg_lo:[1,0]
	v_add_u32_e32 v13, 0x1bd80, v10
	v_pk_fma_f32 v[22:23], v[40:41], v[20:21], v[22:23] op_sel_hi:[0,1,1]
	ds_write_b64 v13, v[22:23]
	v_pk_mul_f32 v[22:23], v[180:181], v[20:21] op_sel:[1,1] op_sel_hi:[0,1] neg_lo:[0,1]
	v_pk_fma_f32 v[20:21], v[180:181], v[20:21], v[22:23] op_sel_hi:[1,0,1]
	v_pk_mul_f32 v[22:23], v[16:17], v[20:21] op_sel:[1,1] op_sel_hi:[1,0] neg_lo:[1,0]
	v_add_u32_e32 v13, 0x1ce00, v10
	v_pk_fma_f32 v[16:17], v[16:17], v[20:21], v[22:23] op_sel_hi:[0,1,1]
	ds_write_b64 v13, v[16:17]
	v_pk_mul_f32 v[16:17], v[180:181], v[20:21] op_sel:[1,1] op_sel_hi:[0,1] neg_lo:[0,1]
	v_pk_fma_f32 v[16:17], v[180:181], v[20:21], v[16:17] op_sel_hi:[1,0,1]
	v_pk_mul_f32 v[20:21], v[30:31], v[16:17] op_sel:[1,1] op_sel_hi:[1,0] neg_lo:[1,0]
	v_add_u32_e32 v13, 0x1de80, v10
	v_pk_fma_f32 v[20:21], v[30:31], v[16:17], v[20:21] op_sel_hi:[0,1,1]
	ds_write_b64 v13, v[20:21]
	v_pk_mul_f32 v[20:21], v[180:181], v[16:17] op_sel:[1,1] op_sel_hi:[0,1] neg_lo:[0,1]
	v_pk_fma_f32 v[16:17], v[180:181], v[16:17], v[20:21] op_sel_hi:[1,0,1]
	v_pk_mul_f32 v[20:21], v[18:19], v[16:17] op_sel:[1,1] op_sel_hi:[1,0] neg_lo:[1,0]
	v_add_u32_e32 v13, 0x1ef00, v10
	v_pk_fma_f32 v[18:19], v[18:19], v[16:17], v[20:21] op_sel_hi:[0,1,1]
	ds_write_b64 v13, v[18:19]
	v_pk_mul_f32 v[18:19], v[180:181], v[16:17] op_sel:[1,1] op_sel_hi:[0,1] neg_lo:[0,1]
	v_pk_fma_f32 v[14:15], v[180:181], v[16:17], v[18:19] op_sel_hi:[1,0,1]
	v_pk_mul_f32 v[16:17], v[34:35], v[14:15] op_sel:[1,1] op_sel_hi:[1,0] neg_lo:[1,0]
	v_add_u32_e32 v10, 0x1ff80, v10
	v_pk_fma_f32 v[14:15], v[34:35], v[14:15], v[16:17] op_sel_hi:[0,1,1]
	ds_write_b64 v10, v[14:15]
	v_mov_b32_e32 v10, v176
	v_mov_b32_e32 v13, v173
	s_waitcnt lgkmcnt(0)
	s_barrier
	v_mov_b32_e32 v14, v182
	v_xad_u32 v28, v13, 3, v10
	v_lshl_add_u32 v71, v28, 3, 0
	v_xad_u32 v28, v13, 4, v10
	v_lshl_add_u32 v70, v28, 3, 0
	v_xad_u32 v28, v13, 5, v10
	v_lshl_add_u32 v69, v28, 3, 0
	v_xad_u32 v28, v13, 6, v10
	v_lshl_add_u32 v68, v28, 3, 0
	v_xad_u32 v28, v13, 7, v10
	v_lshl_add_u32 v67, v28, 3, 0
	v_xad_u32 v28, v13, 8, v10
	v_lshl_add_u32 v28, v28, 3, 0
	v_add_u32_e32 v66, 0x800, v28
	v_xad_u32 v28, v13, 9, v10
	v_lshl_add_u32 v28, v28, 3, 0
	v_add_u32_e32 v65, 0x800, v28
	v_xad_u32 v28, v13, 10, v10
	v_lshl_add_u32 v28, v28, 3, 0
	v_add_u32_e32 v64, 0x800, v28
	v_xad_u32 v28, v13, 11, v10
	v_lshl_add_u32 v28, v28, 3, 0
	v_add_u32_e32 v16, v13, v10
	v_add_u32_e32 v63, 0x800, v28
	v_xad_u32 v28, v13, 12, v10
	v_mov_b32_e32 v15, v183
	v_lshl_add_u32 v74, v16, 3, 0
	v_lshl_add_u32 v28, v28, 3, 0
	ds_read2_b64 v[16:19], v74 offset1:16
	ds_read2_b64 v[38:41], v66 offset1:16
	v_add_u32_e32 v62, 0x800, v28
	v_xad_u32 v28, v13, 13, v10
	v_xad_u32 v20, v13, 1, v10
	v_lshl_add_u32 v28, v28, 3, 0
	v_lshl_add_u32 v73, v20, 3, 0
	v_xad_u32 v24, v13, 2, v10
	v_add_u32_e32 v61, 0x800, v28
	v_xad_u32 v28, v13, 14, v10
	v_xad_u32 v10, v13, 15, v10
	ds_read2_b64 v[20:23], v73 offset0:32 offset1:48
	ds_read2_b64 v[46:49], v65 offset0:32 offset1:48
	v_lshl_add_u32 v28, v28, 3, 0
	v_lshl_add_u32 v10, v10, 3, 0
	v_lshl_add_u32 v72, v24, 3, 0
	v_add_u32_e32 v60, 0x800, v28
	v_add_u32_e32 v13, 0x800, v10
	v_mov_b32_e32 v10, v164
	ds_read2_b64 v[24:27], v72 offset0:64 offset1:80
	ds_read2_b64 v[56:59], v71 offset0:96 offset1:112
	ds_read2_b64 v[76:79], v70 offset0:128 offset1:144
	ds_read2_b64 v[80:83], v69 offset0:160 offset1:176
	ds_read2_b64 v[84:87], v68 offset0:192 offset1:208
	ds_read2_b64 v[88:91], v67 offset0:224 offset1:240
	ds_read2_b64 v[52:55], v64 offset0:64 offset1:80
	ds_read2_b64 v[92:95], v63 offset0:96 offset1:112
	ds_read2_b64 v[96:99], v62 offset0:128 offset1:144
	ds_read2_b64 v[100:103], v61 offset0:160 offset1:176
	ds_read2_b64 v[104:107], v60 offset0:192 offset1:208
	ds_read2_b64 v[108:111], v13 offset0:224 offset1:240
	s_waitcnt lgkmcnt(14)
	v_pk_add_f32 v[112:113], v[16:17], v[38:39]
	v_pk_add_f32 v[38:39], v[16:17], v[38:39] neg_lo:[0,1] neg_hi:[0,1]
	v_pk_add_f32 v[16:17], v[18:19], v[40:41]
	v_pk_add_f32 v[18:19], v[18:19], v[40:41] neg_lo:[0,1] neg_hi:[0,1]
	v_mov_b32_e32 v28, v165
	v_mov_b32_e32 v30, v166
	v_mov_b32_e32 v32, v167
	v_mov_b32_e32 v10, v168
	v_mov_b32_e32 v36, v169
	v_mov_b32_e32 v34, v170
	v_mov_b32_e32 v44, v171
	v_mov_b32_e32 v29, v172
	v_pk_mul_f32 v[40:41], v[18:19], v[44:45] op_sel:[1,0] op_sel_hi:[0,0] neg_lo:[1,1] neg_hi:[0,1]
	v_pk_fma_f32 v[42:43], v[18:19], v[28:29], v[40:41] op_sel_hi:[1,0,1]
	s_waitcnt lgkmcnt(12)
	v_pk_add_f32 v[18:19], v[20:21], v[46:47]
	v_pk_add_f32 v[20:21], v[20:21], v[46:47] neg_lo:[0,1] neg_hi:[0,1]
	v_pk_mul_f32 v[40:41], v[20:21], v[34:35] op_sel:[1,0] op_sel_hi:[0,0] neg_lo:[1,1] neg_hi:[0,1]
	v_pk_fma_f32 v[46:47], v[20:21], v[30:31], v[40:41] op_sel_hi:[1,0,1]
	v_pk_add_f32 v[20:21], v[22:23], v[48:49]
	v_pk_add_f32 v[22:23], v[22:23], v[48:49] neg_lo:[0,1] neg_hi:[0,1]
	v_pk_mul_f32 v[40:41], v[22:23], v[36:37] op_sel:[1,0] op_sel_hi:[0,0] neg_lo:[1,1] neg_hi:[0,1]
	v_pk_fma_f32 v[50:51], v[22:23], v[32:33], v[40:41] op_sel_hi:[1,0,1]
	s_waitcnt lgkmcnt(5)
	v_pk_add_f32 v[22:23], v[24:25], v[52:53]
	v_pk_add_f32 v[24:25], v[24:25], v[52:53] neg_lo:[0,1] neg_hi:[0,1]
	v_pk_mul_f32 v[40:41], v[24:25], v[10:11] op_sel:[1,0] op_sel_hi:[0,0] neg_lo:[1,1] neg_hi:[0,1]
	v_pk_fma_f32 v[52:53], v[24:25], v[10:11], v[40:41] op_sel_hi:[1,0,1]
	v_pk_add_f32 v[24:25], v[26:27], v[54:55]
	v_pk_add_f32 v[26:27], v[26:27], v[54:55] neg_lo:[0,1] neg_hi:[0,1]
	v_pk_mul_f32 v[40:41], v[26:27], v[36:37] op_sel_hi:[1,0]
	v_pk_fma_f32 v[54:55], v[26:27], v[32:33], v[40:41] op_sel:[1,0,0] op_sel_hi:[0,0,1] neg_lo:[1,1,0] neg_hi:[0,1,0]
	s_waitcnt lgkmcnt(4)
	v_pk_add_f32 v[40:41], v[56:57], v[92:93] neg_lo:[0,1] neg_hi:[0,1]
	v_pk_add_f32 v[26:27], v[56:57], v[92:93]
	v_pk_mul_f32 v[48:49], v[40:41], v[34:35] op_sel_hi:[1,0]
	v_pk_fma_f32 v[56:57], v[40:41], v[30:31], v[48:49] op_sel:[1,0,0] op_sel_hi:[0,0,1] neg_lo:[1,1,0] neg_hi:[0,1,0]
	v_pk_add_f32 v[48:49], v[58:59], v[94:95] neg_lo:[0,1] neg_hi:[0,1]
	v_pk_add_f32 v[40:41], v[58:59], v[94:95]
	v_pk_mul_f32 v[58:59], v[48:49], v[44:45] op_sel_hi:[1,0]
	v_xor_b32_e32 v92, 0x80000000, v49
	v_mov_b32_e32 v93, v48
	s_waitcnt lgkmcnt(3)
	v_pk_add_f32 v[48:49], v[76:77], v[96:97]
	v_pk_add_f32 v[76:77], v[76:77], v[96:97] neg_lo:[0,1] neg_hi:[0,1]
	v_pk_fma_f32 v[58:59], v[92:93], v[28:29], v[58:59] op_sel_hi:[1,0,1] neg_lo:[0,1,0] neg_hi:[0,1,0]
	v_xor_b32_e32 v93, 0x80000000, v76
	v_mov_b32_e32 v92, v77
	v_pk_add_f32 v[76:77], v[78:79], v[98:99]
	v_pk_add_f32 v[78:79], v[78:79], v[98:99] neg_lo:[0,1] neg_hi:[0,1]
	v_pk_mul_f32 v[94:95], v[78:79], v[44:45] op_sel_hi:[1,0] neg_lo:[0,1] neg_hi:[0,1]
	v_pk_fma_f32 v[78:79], v[78:79], v[28:29], v[94:95] op_sel:[1,0,0] op_sel_hi:[0,0,1] neg_lo:[1,1,0] neg_hi:[0,1,0]
	s_waitcnt lgkmcnt(2)
	v_pk_add_f32 v[94:95], v[80:81], v[100:101]
	v_pk_add_f32 v[80:81], v[80:81], v[100:101] neg_lo:[0,1] neg_hi:[0,1]
	v_pk_mul_f32 v[96:97], v[80:81], v[34:35] op_sel_hi:[1,0] neg_lo:[0,1] neg_hi:[0,1]
	v_pk_fma_f32 v[80:81], v[80:81], v[30:31], v[96:97] op_sel:[1,0,0] op_sel_hi:[0,0,1] neg_lo:[1,1,0] neg_hi:[0,1,0]
	v_pk_add_f32 v[96:97], v[82:83], v[102:103]
	v_pk_add_f32 v[82:83], v[82:83], v[102:103] neg_lo:[0,1] neg_hi:[0,1]
	v_pk_mul_f32 v[98:99], v[82:83], v[36:37] op_sel_hi:[1,0] neg_lo:[0,1] neg_hi:[0,1]
	v_pk_fma_f32 v[82:83], v[82:83], v[32:33], v[98:99] op_sel:[1,0,0] op_sel_hi:[0,0,1] neg_lo:[1,1,0] neg_hi:[0,1,0]
	s_waitcnt lgkmcnt(1)
	v_pk_add_f32 v[98:99], v[84:85], v[104:105]
	v_pk_add_f32 v[84:85], v[84:85], v[104:105] neg_lo:[0,1] neg_hi:[0,1]
	v_pk_mul_f32 v[100:101], v[84:85], v[10:11] op_sel:[1,0] op_sel_hi:[0,0] neg_lo:[1,1] neg_hi:[0,1]
	v_pk_fma_f32 v[84:85], v[84:85], v[10:11], v[100:101] op_sel_hi:[1,0,1] neg_lo:[0,1,0] neg_hi:[0,1,0]
	v_pk_add_f32 v[100:101], v[86:87], v[106:107]
	v_pk_add_f32 v[86:87], v[86:87], v[106:107] neg_lo:[0,1] neg_hi:[0,1]
	v_pk_mul_f32 v[36:37], v[86:87], v[36:37] op_sel:[1,0] op_sel_hi:[0,0] neg_lo:[1,1] neg_hi:[0,1]
	v_pk_fma_f32 v[86:87], v[86:87], v[32:33], v[36:37] op_sel_hi:[1,0,1] neg_lo:[0,1,0] neg_hi:[0,1,0]
	s_waitcnt lgkmcnt(0)
	v_pk_add_f32 v[36:37], v[88:89], v[108:109] neg_lo:[0,1] neg_hi:[0,1]
	v_pk_add_f32 v[32:33], v[88:89], v[108:109]
	v_pk_mul_f32 v[88:89], v[36:37], v[34:35] op_sel:[1,0] op_sel_hi:[0,0] neg_lo:[1,1] neg_hi:[0,1]
	v_pk_fma_f32 v[88:89], v[36:37], v[30:31], v[88:89] op_sel_hi:[1,0,1] neg_lo:[0,1,0] neg_hi:[0,1,0]
	v_pk_add_f32 v[36:37], v[90:91], v[110:111]
	v_pk_add_f32 v[90:91], v[90:91], v[110:111] neg_lo:[0,1] neg_hi:[0,1]
	v_pk_mul_f32 v[44:45], v[90:91], v[44:45] op_sel:[1,0] op_sel_hi:[0,0] neg_lo:[1,1] neg_hi:[0,1]
	v_pk_fma_f32 v[90:91], v[90:91], v[28:29], v[44:45] op_sel_hi:[1,0,1] neg_lo:[0,1,0] neg_hi:[0,1,0]
	v_pk_add_f32 v[44:45], v[16:17], v[76:77]
	v_pk_add_f32 v[16:17], v[16:17], v[76:77] neg_lo:[0,1] neg_hi:[0,1]
	v_pk_add_f32 v[28:29], v[112:113], v[48:49]
	v_pk_mul_f32 v[76:77], v[16:17], v[34:35] op_sel:[1,0] op_sel_hi:[0,0] neg_lo:[1,1] neg_hi:[0,1]
	v_pk_add_f32 v[48:49], v[112:113], v[48:49] neg_lo:[0,1] neg_hi:[0,1]
	v_pk_fma_f32 v[76:77], v[16:17], v[30:31], v[76:77] op_sel_hi:[1,0,1]
	v_pk_add_f32 v[16:17], v[18:19], v[94:95]
	v_pk_add_f32 v[18:19], v[18:19], v[94:95] neg_lo:[0,1] neg_hi:[0,1]
	v_pk_mul_f32 v[94:95], v[18:19], v[10:11] op_sel:[1,0] op_sel_hi:[0,0] neg_lo:[1,1] neg_hi:[0,1]
	v_pk_fma_f32 v[18:19], v[18:19], v[10:11], v[94:95] op_sel_hi:[1,0,1]
	v_pk_add_f32 v[94:95], v[20:21], v[96:97]
	v_pk_add_f32 v[20:21], v[20:21], v[96:97] neg_lo:[0,1] neg_hi:[0,1]
	v_pk_mul_f32 v[96:97], v[20:21], v[34:35] op_sel_hi:[1,0]
	v_xor_b32_e32 v102, 0x80000000, v21
	v_mov_b32_e32 v103, v20
	v_pk_add_f32 v[20:21], v[22:23], v[98:99]
	v_pk_add_f32 v[22:23], v[22:23], v[98:99] neg_lo:[0,1] neg_hi:[0,1]
	v_pk_fma_f32 v[96:97], v[102:103], v[30:31], v[96:97] op_sel_hi:[1,0,1] neg_lo:[0,1,0] neg_hi:[0,1,0]
	v_xor_b32_e32 v99, 0x80000000, v22
	v_mov_b32_e32 v98, v23
	v_pk_add_f32 v[22:23], v[24:25], v[100:101]
	v_pk_add_f32 v[24:25], v[24:25], v[100:101] neg_lo:[0,1] neg_hi:[0,1]
	v_pk_mul_f32 v[100:101], v[24:25], v[34:35] op_sel_hi:[1,0] neg_lo:[0,1] neg_hi:[0,1]
	v_xor_b32_e32 v102, 0x80000000, v25
	v_mov_b32_e32 v103, v24
	v_pk_add_f32 v[24:25], v[26:27], v[32:33]
	v_pk_add_f32 v[26:27], v[26:27], v[32:33] neg_lo:[0,1] neg_hi:[0,1]
	v_pk_fma_f32 v[100:101], v[102:103], v[30:31], v[100:101] op_sel_hi:[1,0,1] neg_lo:[0,1,0] neg_hi:[0,1,0]
	v_pk_mul_f32 v[32:33], v[26:27], v[10:11] op_sel:[1,0] op_sel_hi:[0,0] neg_lo:[1,1] neg_hi:[0,1]
	v_pk_add_f32 v[102:103], v[28:29], v[20:21] neg_lo:[0,1] neg_hi:[0,1]
	v_pk_fma_f32 v[26:27], v[26:27], v[10:11], v[32:33] op_sel_hi:[1,0,1] neg_lo:[0,1,0] neg_hi:[0,1,0]
	v_pk_add_f32 v[32:33], v[40:41], v[36:37]
	v_pk_add_f32 v[36:37], v[40:41], v[36:37] neg_lo:[0,1] neg_hi:[0,1]
	v_pk_mul_f32 v[40:41], v[36:37], v[34:35] op_sel:[1,0] op_sel_hi:[0,0] neg_lo:[1,1] neg_hi:[0,1]
	v_pk_fma_f32 v[40:41], v[36:37], v[30:31], v[40:41] op_sel_hi:[1,0,1] neg_lo:[0,1,0] neg_hi:[0,1,0]
	v_pk_add_f32 v[36:37], v[28:29], v[20:21]
	v_pk_add_f32 v[20:21], v[44:45], v[22:23]
	v_pk_add_f32 v[22:23], v[44:45], v[22:23] neg_lo:[0,1] neg_hi:[0,1]
	v_pk_mul_f32 v[28:29], v[22:23], v[10:11] op_sel:[1,0] op_sel_hi:[0,0] neg_lo:[1,1] neg_hi:[0,1]
	v_pk_fma_f32 v[22:23], v[22:23], v[10:11], v[28:29] op_sel_hi:[1,0,1]
	v_pk_add_f32 v[28:29], v[16:17], v[24:25]
	v_pk_add_f32 v[16:17], v[16:17], v[24:25] neg_lo:[0,1] neg_hi:[0,1]
	v_xor_b32_e32 v25, 0x80000000, v16
	v_mov_b32_e32 v24, v17
	v_pk_add_f32 v[16:17], v[94:95], v[32:33]
	v_pk_add_f32 v[32:33], v[94:95], v[32:33] neg_lo:[0,1] neg_hi:[0,1]
	v_pk_mul_f32 v[44:45], v[32:33], v[10:11] op_sel:[1,0] op_sel_hi:[0,0] neg_lo:[1,1] neg_hi:[0,1]
	v_pk_fma_f32 v[32:33], v[32:33], v[10:11], v[44:45] op_sel_hi:[1,0,1] neg_lo:[0,1,0] neg_hi:[0,1,0]
	v_pk_add_f32 v[44:45], v[36:37], v[28:29]
	v_pk_add_f32 v[36:37], v[36:37], v[28:29] neg_lo:[0,1] neg_hi:[0,1]
	v_pk_add_f32 v[28:29], v[20:21], v[16:17]
	v_pk_add_f32 v[16:17], v[20:21], v[16:17] neg_lo:[0,1] neg_hi:[0,1]
	v_pk_add_f32 v[94:95], v[44:45], v[28:29]
	v_xor_b32_e32 v21, 0x80000000, v16
	v_mov_b32_e32 v20, v17
	v_pk_add_f32 v[16:17], v[102:103], v[24:25]
	v_pk_add_f32 v[102:103], v[102:103], v[24:25] neg_lo:[0,1] neg_hi:[0,1]
	v_pk_add_f32 v[24:25], v[22:23], v[32:33]
	v_pk_add_f32 v[22:23], v[22:23], v[32:33] neg_lo:[0,1] neg_hi:[0,1]
	v_pk_add_f32 v[28:29], v[44:45], v[28:29] neg_lo:[0,1] neg_hi:[0,1]
	v_xor_b32_e32 v33, 0x80000000, v22
	v_mov_b32_e32 v32, v23
	v_pk_add_f32 v[22:23], v[48:49], v[98:99]
	v_pk_add_f32 v[98:99], v[48:49], v[98:99] neg_lo:[0,1] neg_hi:[0,1]
	v_pk_add_f32 v[48:49], v[76:77], v[100:101] neg_lo:[0,1] neg_hi:[0,1]
	v_pk_add_f32 v[44:45], v[36:37], v[20:21]
	v_pk_add_f32 v[20:21], v[36:37], v[20:21] neg_lo:[0,1] neg_hi:[0,1]
	v_pk_add_f32 v[104:105], v[16:17], v[24:25]
	v_pk_add_f32 v[24:25], v[16:17], v[24:25] neg_lo:[0,1] neg_hi:[0,1]
	v_pk_add_f32 v[36:37], v[102:103], v[32:33]
	v_pk_add_f32 v[16:17], v[102:103], v[32:33] neg_lo:[0,1] neg_hi:[0,1]
	v_pk_add_f32 v[32:33], v[76:77], v[100:101]
	v_pk_mul_f32 v[76:77], v[10:11], v[48:49] op_sel:[0,1] op_sel_hi:[0,0] neg_lo:[1,1] neg_hi:[1,0]
	v_pk_fma_f32 v[76:77], v[10:11], v[48:49], v[76:77] op_sel_hi:[0,1,1]
	v_pk_add_f32 v[48:49], v[18:19], v[26:27]
	v_pk_add_f32 v[18:19], v[18:19], v[26:27] neg_lo:[0,1] neg_hi:[0,1]
	v_xor_b32_e32 v27, 0x80000000, v18
	v_mov_b32_e32 v26, v19
	v_pk_add_f32 v[18:19], v[96:97], v[40:41]
	v_pk_add_f32 v[40:41], v[96:97], v[40:41] neg_lo:[0,1] neg_hi:[0,1]
	v_pk_mul_f32 v[96:97], v[10:11], v[40:41] op_sel:[0,1] op_sel_hi:[0,0] neg_lo:[1,1] neg_hi:[1,0]
	v_pk_fma_f32 v[40:41], v[10:11], v[40:41], v[96:97] op_sel_hi:[0,1,1] neg_lo:[1,0,0] neg_hi:[1,0,0]
	v_pk_add_f32 v[96:97], v[22:23], v[48:49]
	v_pk_add_f32 v[22:23], v[22:23], v[48:49] neg_lo:[0,1] neg_hi:[0,1]
	v_pk_add_f32 v[48:49], v[32:33], v[18:19]
	v_pk_add_f32 v[18:19], v[32:33], v[18:19] neg_lo:[0,1] neg_hi:[0,1]
	v_pk_add_f32 v[102:103], v[96:97], v[48:49]
	v_xor_b32_e32 v101, 0x80000000, v18
	v_mov_b32_e32 v100, v19
	v_pk_add_f32 v[32:33], v[96:97], v[48:49] neg_lo:[0,1] neg_hi:[0,1]
	v_pk_add_f32 v[18:19], v[98:99], v[26:27]
	v_pk_add_f32 v[96:97], v[98:99], v[26:27] neg_lo:[0,1] neg_hi:[0,1]
	v_pk_add_f32 v[26:27], v[76:77], v[40:41]
	v_pk_add_f32 v[40:41], v[76:77], v[40:41] neg_lo:[0,1] neg_hi:[0,1]
	v_pk_add_f32 v[98:99], v[18:19], v[26:27]
	v_xor_b32_e32 v77, 0x80000000, v40
	v_mov_b32_e32 v76, v41
	v_pk_add_f32 v[26:27], v[18:19], v[26:27] neg_lo:[0,1] neg_hi:[0,1]
	v_pk_add_f32 v[40:41], v[96:97], v[76:77]
	v_pk_add_f32 v[18:19], v[96:97], v[76:77] neg_lo:[0,1] neg_hi:[0,1]
	v_pk_add_f32 v[76:77], v[38:39], v[92:93]
	v_pk_add_f32 v[92:93], v[38:39], v[92:93] neg_lo:[0,1] neg_hi:[0,1]
	v_pk_add_f32 v[38:39], v[42:43], v[78:79]
	v_pk_add_f32 v[42:43], v[42:43], v[78:79] neg_lo:[0,1] neg_hi:[0,1]
	v_pk_add_f32 v[48:49], v[22:23], v[100:101]
	v_pk_mul_f32 v[78:79], v[34:35], v[42:43] op_sel:[0,1] op_sel_hi:[0,0] neg_lo:[1,1] neg_hi:[1,0]
	v_pk_fma_f32 v[42:43], v[30:31], v[42:43], v[78:79] op_sel_hi:[0,1,1]
	v_pk_add_f32 v[78:79], v[46:47], v[80:81]
	v_pk_add_f32 v[46:47], v[46:47], v[80:81] neg_lo:[0,1] neg_hi:[0,1]
	v_pk_add_f32 v[22:23], v[22:23], v[100:101] neg_lo:[0,1] neg_hi:[0,1]
	v_pk_mul_f32 v[80:81], v[10:11], v[46:47] op_sel:[0,1] op_sel_hi:[0,0] neg_lo:[1,1] neg_hi:[1,0]
	v_pk_fma_f32 v[80:81], v[10:11], v[46:47], v[80:81] op_sel_hi:[0,1,1]
	v_pk_add_f32 v[46:47], v[50:51], v[82:83]
	v_pk_add_f32 v[50:51], v[50:51], v[82:83] neg_lo:[0,1] neg_hi:[0,1]
	v_pk_mul_f32 v[82:83], v[30:31], v[50:51] op_sel:[0,1] op_sel_hi:[0,0] neg_lo:[1,1] neg_hi:[1,0]
	v_pk_fma_f32 v[50:51], v[34:35], v[50:51], v[82:83] op_sel_hi:[0,1,1]
	v_pk_add_f32 v[82:83], v[52:53], v[84:85]
	v_pk_add_f32 v[52:53], v[52:53], v[84:85] neg_lo:[0,1] neg_hi:[0,1]
	v_xor_b32_e32 v85, 0x80000000, v52
	v_mov_b32_e32 v84, v53
	v_pk_add_f32 v[52:53], v[54:55], v[86:87]
	v_pk_add_f32 v[54:55], v[54:55], v[86:87] neg_lo:[0,1] neg_hi:[0,1]
	v_pk_mul_f32 v[86:87], v[30:31], v[54:55] op_sel:[0,1] op_sel_hi:[0,0] neg_lo:[1,1] neg_hi:[1,0]
	v_pk_fma_f32 v[54:55], v[34:35], v[54:55], v[86:87] op_sel_hi:[0,1,1] neg_lo:[1,0,0] neg_hi:[1,0,0]
	v_pk_add_f32 v[86:87], v[56:57], v[88:89]
	v_pk_add_f32 v[56:57], v[56:57], v[88:89] neg_lo:[0,1] neg_hi:[0,1]
	v_pk_mul_f32 v[88:89], v[10:11], v[56:57] op_sel:[0,1] op_sel_hi:[0,0] neg_lo:[1,1] neg_hi:[1,0]
	v_pk_fma_f32 v[56:57], v[10:11], v[56:57], v[88:89] op_sel_hi:[0,1,1] neg_lo:[1,0,0] neg_hi:[1,0,0]
	v_pk_add_f32 v[88:89], v[58:59], v[90:91]
	v_pk_add_f32 v[58:59], v[58:59], v[90:91] neg_lo:[0,1] neg_hi:[0,1]
	v_pk_mul_f32 v[34:35], v[34:35], v[58:59] op_sel:[0,1] op_sel_hi:[0,0] neg_lo:[1,1] neg_hi:[1,0]
	v_pk_fma_f32 v[34:35], v[30:31], v[58:59], v[34:35] op_sel_hi:[0,1,1] neg_lo:[1,0,0] neg_hi:[1,0,0]
	v_pk_add_f32 v[30:31], v[76:77], v[82:83]
	v_pk_add_f32 v[58:59], v[76:77], v[82:83] neg_lo:[0,1] neg_hi:[0,1]
	v_pk_add_f32 v[76:77], v[52:53], v[38:39]
	v_pk_add_f32 v[38:39], v[38:39], v[52:53] neg_lo:[0,1] neg_hi:[0,1]
	v_pk_mul_f32 v[52:53], v[10:11], v[38:39] op_sel:[0,1] op_sel_hi:[0,0] neg_lo:[1,1] neg_hi:[1,0]
	v_pk_fma_f32 v[52:53], v[10:11], v[38:39], v[52:53] op_sel_hi:[0,1,1]
	v_pk_add_f32 v[38:39], v[78:79], v[86:87]
	v_pk_add_f32 v[78:79], v[78:79], v[86:87] neg_lo:[0,1] neg_hi:[0,1]
	v_xor_b32_e32 v83, 0x80000000, v78
	v_mov_b32_e32 v82, v79
	v_pk_add_f32 v[78:79], v[46:47], v[88:89]
	v_pk_add_f32 v[46:47], v[46:47], v[88:89] neg_lo:[0,1] neg_hi:[0,1]
	v_pk_add_f32 v[88:89], v[76:77], v[78:79]
	v_pk_mul_f32 v[86:87], v[10:11], v[46:47] op_sel:[0,1] op_sel_hi:[0,0] neg_lo:[1,1] neg_hi:[1,0]
	v_pk_fma_f32 v[46:47], v[10:11], v[46:47], v[86:87] op_sel_hi:[0,1,1] neg_lo:[1,0,0] neg_hi:[1,0,0]
	v_pk_add_f32 v[86:87], v[30:31], v[38:39]
	v_pk_add_f32 v[30:31], v[30:31], v[38:39] neg_lo:[0,1] neg_hi:[0,1]
	v_pk_add_f32 v[38:39], v[76:77], v[78:79] neg_lo:[0,1] neg_hi:[0,1]
	v_pk_add_f32 v[78:79], v[86:87], v[88:89] neg_lo:[0,1] neg_hi:[0,1]
	v_pk_add_f32 v[90:91], v[30:31], v[38:39] op_sel:[0,1] op_sel_hi:[1,0] neg_hi:[0,1]
	v_pk_add_f32 v[38:39], v[30:31], v[38:39] op_sel:[0,1] op_sel_hi:[1,0] neg_lo:[0,1]
	v_pk_add_f32 v[76:77], v[52:53], v[46:47]
	v_pk_add_f32 v[46:47], v[52:53], v[46:47] neg_lo:[0,1] neg_hi:[0,1]
	v_pk_add_f32 v[30:31], v[58:59], v[82:83]
	v_pk_add_f32 v[58:59], v[58:59], v[82:83] neg_lo:[0,1] neg_hi:[0,1]
	v_xor_b32_e32 v53, 0x80000000, v46
	v_mov_b32_e32 v52, v47
	v_pk_add_f32 v[82:83], v[30:31], v[76:77]
	v_pk_add_f32 v[46:47], v[30:31], v[76:77] neg_lo:[0,1] neg_hi:[0,1]
	v_pk_add_f32 v[76:77], v[58:59], v[52:53]
	v_pk_add_f32 v[30:31], v[58:59], v[52:53] neg_lo:[0,1] neg_hi:[0,1]
	v_pk_add_f32 v[52:53], v[92:93], v[84:85]
	v_pk_add_f32 v[58:59], v[92:93], v[84:85] neg_lo:[0,1] neg_hi:[0,1]
	v_pk_add_f32 v[84:85], v[54:55], v[42:43]
	v_pk_add_f32 v[42:43], v[42:43], v[54:55] neg_lo:[0,1] neg_hi:[0,1]
	v_pk_add_f32 v[86:87], v[86:87], v[88:89]
	v_pk_mul_f32 v[54:55], v[10:11], v[42:43] op_sel:[0,1] op_sel_hi:[0,0] neg_lo:[1,1] neg_hi:[1,0]
	v_pk_fma_f32 v[54:55], v[10:11], v[42:43], v[54:55] op_sel_hi:[0,1,1]
	v_pk_add_f32 v[42:43], v[80:81], v[56:57]
	v_pk_add_f32 v[56:57], v[80:81], v[56:57] neg_lo:[0,1] neg_hi:[0,1]
	v_xor_b32_e32 v81, 0x80000000, v56
	v_mov_b32_e32 v80, v57
	v_pk_add_f32 v[56:57], v[50:51], v[34:35]
	v_pk_add_f32 v[34:35], v[50:51], v[34:35] neg_lo:[0,1] neg_hi:[0,1]
	v_pk_mul_f32 v[50:51], v[10:11], v[34:35] op_sel:[0,1] op_sel_hi:[0,0] neg_lo:[1,1] neg_hi:[1,0]
	v_pk_fma_f32 v[34:35], v[10:11], v[34:35], v[50:51] op_sel_hi:[0,1,1] neg_lo:[1,0,0] neg_hi:[1,0,0]
	v_pk_add_f32 v[50:51], v[52:53], v[42:43]
	v_pk_add_f32 v[42:43], v[52:53], v[42:43] neg_lo:[0,1] neg_hi:[0,1]
	v_pk_add_f32 v[52:53], v[84:85], v[56:57]
	v_pk_add_f32 v[56:57], v[84:85], v[56:57] neg_lo:[0,1] neg_hi:[0,1]
	v_xor_b32_e32 v85, 0x80000000, v56
	v_mov_b32_e32 v84, v57
	v_pk_add_f32 v[56:57], v[50:51], v[52:53]
	v_pk_add_f32 v[50:51], v[50:51], v[52:53] neg_lo:[0,1] neg_hi:[0,1]
	v_pk_add_f32 v[52:53], v[42:43], v[84:85]
	v_pk_add_f32 v[42:43], v[42:43], v[84:85] neg_lo:[0,1] neg_hi:[0,1]
	v_pk_add_f32 v[84:85], v[58:59], v[80:81]
	v_pk_add_f32 v[58:59], v[58:59], v[80:81] neg_lo:[0,1] neg_hi:[0,1]
	v_pk_add_f32 v[80:81], v[54:55], v[34:35]
	v_pk_add_f32 v[34:35], v[54:55], v[34:35] neg_lo:[0,1] neg_hi:[0,1]
	v_pk_add_f32 v[92:93], v[84:85], v[80:81]
	v_pk_add_f32 v[80:81], v[84:85], v[80:81] neg_lo:[0,1] neg_hi:[0,1]
	v_pk_add_f32 v[84:85], v[58:59], v[34:35] op_sel:[0,1] op_sel_hi:[1,0] neg_hi:[0,1]
	v_pk_add_f32 v[34:35], v[58:59], v[34:35] op_sel:[0,1] op_sel_hi:[1,0] neg_lo:[0,1]
	v_pk_fma_f32 v[58:59], v[14:15], s[92:93], v[14:15] op_sel:[1,0,0] op_sel_hi:[0,1,1]
	v_pk_mul_f32 v[54:55], v[94:95], s[14:15] op_sel:[1,0] neg_lo:[1,0]
	v_pk_mul_f32 v[88:89], v[58:59], v[86:87] op_sel:[1,1] op_sel_hi:[0,1] neg_lo:[0,1]
	v_pk_fma_f32 v[54:55], v[94:95], s[42:43], v[54:55] op_sel_hi:[0,1,1]
	v_pk_fma_f32 v[86:87], v[58:59], v[86:87], v[88:89] op_sel_hi:[1,0,1]
	ds_write2_b64 v74, v[54:55], v[86:87] offset1:16
	v_pk_mul_f32 v[54:55], v[14:15], v[58:59] op_sel:[1,1] op_sel_hi:[0,1] neg_lo:[0,1]
	v_pk_fma_f32 v[54:55], v[14:15], v[58:59], v[54:55] op_sel_hi:[1,0,1]
	v_pk_mul_f32 v[58:59], v[54:55], v[102:103] op_sel:[1,1] op_sel_hi:[0,1] neg_lo:[0,1]
	v_pk_mul_f32 v[74:75], v[14:15], v[54:55] op_sel:[1,1] op_sel_hi:[0,1] neg_lo:[0,1]
	v_pk_fma_f32 v[58:59], v[54:55], v[102:103], v[58:59] op_sel_hi:[1,0,1]
	v_pk_fma_f32 v[54:55], v[14:15], v[54:55], v[74:75] op_sel_hi:[1,0,1]
	v_pk_mul_f32 v[74:75], v[54:55], v[56:57] op_sel:[1,1] op_sel_hi:[0,1] neg_lo:[0,1]
	v_pk_fma_f32 v[56:57], v[54:55], v[56:57], v[74:75] op_sel_hi:[1,0,1]
	ds_write2_b64 v73, v[58:59], v[56:57] offset0:32 offset1:48
	v_pk_mul_f32 v[56:57], v[14:15], v[54:55] op_sel:[1,1] op_sel_hi:[0,1] neg_lo:[0,1]
	v_pk_fma_f32 v[54:55], v[14:15], v[54:55], v[56:57] op_sel_hi:[1,0,1]
	v_pk_mul_f32 v[56:57], v[54:55], v[104:105] op_sel:[1,1] op_sel_hi:[0,1] neg_lo:[0,1]
	v_pk_mul_f32 v[58:59], v[14:15], v[54:55] op_sel:[1,1] op_sel_hi:[0,1] neg_lo:[0,1]
	v_pk_fma_f32 v[56:57], v[54:55], v[104:105], v[56:57] op_sel_hi:[1,0,1]
	v_pk_fma_f32 v[54:55], v[14:15], v[54:55], v[58:59] op_sel_hi:[1,0,1]
	v_pk_mul_f32 v[58:59], v[54:55], v[82:83] op_sel:[1,1] op_sel_hi:[0,1] neg_lo:[0,1]
	v_pk_fma_f32 v[58:59], v[54:55], v[82:83], v[58:59] op_sel_hi:[1,0,1]
	ds_write2_b64 v72, v[56:57], v[58:59] offset0:64 offset1:80
	v_pk_mul_f32 v[56:57], v[14:15], v[54:55] op_sel:[1,1] op_sel_hi:[0,1] neg_lo:[0,1]
	v_pk_fma_f32 v[54:55], v[14:15], v[54:55], v[56:57] op_sel_hi:[1,0,1]
	v_pk_mul_f32 v[56:57], v[54:55], v[98:99] op_sel:[1,1] op_sel_hi:[0,1] neg_lo:[0,1]
	v_pk_mul_f32 v[58:59], v[14:15], v[54:55] op_sel:[1,1] op_sel_hi:[0,1] neg_lo:[0,1]
	v_pk_fma_f32 v[56:57], v[54:55], v[98:99], v[56:57] op_sel_hi:[1,0,1]
	v_pk_fma_f32 v[54:55], v[14:15], v[54:55], v[58:59] op_sel_hi:[1,0,1]
	v_pk_mul_f32 v[58:59], v[54:55], v[92:93] op_sel:[1,1] op_sel_hi:[0,1] neg_lo:[0,1]
	v_pk_fma_f32 v[58:59], v[54:55], v[92:93], v[58:59] op_sel_hi:[1,0,1]
	ds_write2_b64 v71, v[56:57], v[58:59] offset0:96 offset1:112
	v_pk_mul_f32 v[56:57], v[14:15], v[54:55] op_sel:[1,1] op_sel_hi:[0,1] neg_lo:[0,1]
	v_pk_fma_f32 v[54:55], v[14:15], v[54:55], v[56:57] op_sel_hi:[1,0,1]
	v_pk_mul_f32 v[56:57], v[54:55], v[44:45] op_sel:[1,1] op_sel_hi:[0,1] neg_lo:[0,1]
	v_pk_fma_f32 v[44:45], v[54:55], v[44:45], v[56:57] op_sel_hi:[1,0,1]
	v_pk_mul_f32 v[56:57], v[14:15], v[54:55] op_sel:[1,1] op_sel_hi:[0,1] neg_lo:[0,1]
	v_pk_fma_f32 v[54:55], v[14:15], v[54:55], v[56:57] op_sel_hi:[1,0,1]
	v_pk_mul_f32 v[56:57], v[54:55], v[90:91] op_sel:[1,1] op_sel_hi:[0,1] neg_lo:[0,1]
	v_pk_fma_f32 v[56:57], v[54:55], v[90:91], v[56:57] op_sel_hi:[1,0,1]
	ds_write2_b64 v70, v[44:45], v[56:57] offset0:128 offset1:144
	v_pk_mul_f32 v[44:45], v[14:15], v[54:55] op_sel:[1,1] op_sel_hi:[0,1] neg_lo:[0,1]
	v_pk_fma_f32 v[44:45], v[14:15], v[54:55], v[44:45] op_sel_hi:[1,0,1]
	v_pk_mul_f32 v[54:55], v[44:45], v[48:49] op_sel:[1,1] op_sel_hi:[0,1] neg_lo:[0,1]
	v_pk_fma_f32 v[48:49], v[44:45], v[48:49], v[54:55] op_sel_hi:[1,0,1]
	v_pk_mul_f32 v[54:55], v[14:15], v[44:45] op_sel:[1,1] op_sel_hi:[0,1] neg_lo:[0,1]
	v_pk_fma_f32 v[44:45], v[14:15], v[44:45], v[54:55] op_sel_hi:[1,0,1]
	v_pk_mul_f32 v[54:55], v[44:45], v[52:53] op_sel:[1,1] op_sel_hi:[0,1] neg_lo:[0,1]
	v_pk_fma_f32 v[52:53], v[44:45], v[52:53], v[54:55] op_sel_hi:[1,0,1]
	ds_write2_b64 v69, v[48:49], v[52:53] offset0:160 offset1:176
	v_pk_mul_f32 v[48:49], v[14:15], v[44:45] op_sel:[1,1] op_sel_hi:[0,1] neg_lo:[0,1]
	v_pk_fma_f32 v[44:45], v[14:15], v[44:45], v[48:49] op_sel_hi:[1,0,1]
	v_pk_mul_f32 v[48:49], v[36:37], v[44:45] op_sel:[1,1] op_sel_hi:[1,0] neg_lo:[1,0]
	v_pk_fma_f32 v[36:37], v[36:37], v[44:45], v[48:49] op_sel_hi:[0,1,1]
	v_pk_mul_f32 v[48:49], v[14:15], v[44:45] op_sel:[1,1] op_sel_hi:[0,1] neg_lo:[0,1]
	v_pk_fma_f32 v[44:45], v[14:15], v[44:45], v[48:49] op_sel_hi:[1,0,1]
	v_pk_mul_f32 v[48:49], v[44:45], v[76:77] op_sel:[1,1] op_sel_hi:[0,1] neg_lo:[0,1]
	v_pk_fma_f32 v[48:49], v[44:45], v[76:77], v[48:49] op_sel_hi:[1,0,1]
	ds_write2_b64 v68, v[36:37], v[48:49] offset0:192 offset1:208
	v_pk_mul_f32 v[36:37], v[14:15], v[44:45] op_sel:[1,1] op_sel_hi:[0,1] neg_lo:[0,1]
	v_pk_fma_f32 v[36:37], v[14:15], v[44:45], v[36:37] op_sel_hi:[1,0,1]
	v_pk_mul_f32 v[44:45], v[40:41], v[36:37] op_sel:[1,1] op_sel_hi:[1,0] neg_lo:[1,0]
	v_pk_fma_f32 v[40:41], v[40:41], v[36:37], v[44:45] op_sel_hi:[0,1,1]
	v_pk_mul_f32 v[44:45], v[14:15], v[36:37] op_sel:[1,1] op_sel_hi:[0,1] neg_lo:[0,1]
	v_pk_fma_f32 v[36:37], v[14:15], v[36:37], v[44:45] op_sel_hi:[1,0,1]
	v_pk_mul_f32 v[44:45], v[36:37], v[84:85] op_sel:[1,1] op_sel_hi:[0,1] neg_lo:[0,1]
	v_pk_fma_f32 v[44:45], v[36:37], v[84:85], v[44:45] op_sel_hi:[1,0,1]
	ds_write2_b64 v67, v[40:41], v[44:45] offset0:224 offset1:240
	v_pk_mul_f32 v[40:41], v[14:15], v[36:37] op_sel:[1,1] op_sel_hi:[0,1] neg_lo:[0,1]
	v_pk_fma_f32 v[36:37], v[14:15], v[36:37], v[40:41] op_sel_hi:[1,0,1]
	v_pk_mul_f32 v[40:41], v[28:29], v[36:37] op_sel:[1,1] op_sel_hi:[1,0] neg_lo:[1,0]
	v_pk_fma_f32 v[28:29], v[28:29], v[36:37], v[40:41] op_sel_hi:[0,1,1]
	v_pk_mul_f32 v[40:41], v[14:15], v[36:37] op_sel:[1,1] op_sel_hi:[0,1] neg_lo:[0,1]
	v_pk_fma_f32 v[36:37], v[14:15], v[36:37], v[40:41] op_sel_hi:[1,0,1]
	v_pk_mul_f32 v[40:41], v[78:79], v[36:37] op_sel:[1,1] op_sel_hi:[1,0] neg_lo:[1,0]
	v_pk_fma_f32 v[40:41], v[78:79], v[36:37], v[40:41] op_sel_hi:[0,1,1]
	ds_write2_b64 v66, v[28:29], v[40:41] offset1:16
	v_pk_mul_f32 v[28:29], v[14:15], v[36:37] op_sel:[1,1] op_sel_hi:[0,1] neg_lo:[0,1]
	v_pk_fma_f32 v[28:29], v[14:15], v[36:37], v[28:29] op_sel_hi:[1,0,1]
	v_pk_mul_f32 v[36:37], v[32:33], v[28:29] op_sel:[1,1] op_sel_hi:[1,0] neg_lo:[1,0]
	v_pk_fma_f32 v[32:33], v[32:33], v[28:29], v[36:37] op_sel_hi:[0,1,1]
	v_pk_mul_f32 v[36:37], v[14:15], v[28:29] op_sel:[1,1] op_sel_hi:[0,1] neg_lo:[0,1]
	v_pk_fma_f32 v[28:29], v[14:15], v[28:29], v[36:37] op_sel_hi:[1,0,1]
	v_pk_mul_f32 v[36:37], v[50:51], v[28:29] op_sel:[1,1] op_sel_hi:[1,0] neg_lo:[1,0]
	v_pk_fma_f32 v[36:37], v[50:51], v[28:29], v[36:37] op_sel_hi:[0,1,1]
	ds_write2_b64 v65, v[32:33], v[36:37] offset0:32 offset1:48
	v_pk_mul_f32 v[32:33], v[14:15], v[28:29] op_sel:[1,1] op_sel_hi:[0,1] neg_lo:[0,1]
	v_pk_fma_f32 v[28:29], v[14:15], v[28:29], v[32:33] op_sel_hi:[1,0,1]
	v_pk_mul_f32 v[32:33], v[24:25], v[28:29] op_sel:[1,1] op_sel_hi:[1,0] neg_lo:[1,0]
	v_pk_fma_f32 v[24:25], v[24:25], v[28:29], v[32:33] op_sel_hi:[0,1,1]
	v_pk_mul_f32 v[32:33], v[14:15], v[28:29] op_sel:[1,1] op_sel_hi:[0,1] neg_lo:[0,1]
	v_pk_fma_f32 v[28:29], v[14:15], v[28:29], v[32:33] op_sel_hi:[1,0,1]
	v_pk_mul_f32 v[32:33], v[46:47], v[28:29] op_sel:[1,1] op_sel_hi:[1,0] neg_lo:[1,0]
	v_pk_fma_f32 v[32:33], v[46:47], v[28:29], v[32:33] op_sel_hi:[0,1,1]
	ds_write2_b64 v64, v[24:25], v[32:33] offset0:64 offset1:80
	v_pk_mul_f32 v[24:25], v[14:15], v[28:29] op_sel:[1,1] op_sel_hi:[0,1] neg_lo:[0,1]
	v_pk_fma_f32 v[24:25], v[14:15], v[28:29], v[24:25] op_sel_hi:[1,0,1]
	v_pk_mul_f32 v[28:29], v[26:27], v[24:25] op_sel:[1,1] op_sel_hi:[1,0] neg_lo:[1,0]
	v_pk_fma_f32 v[26:27], v[26:27], v[24:25], v[28:29] op_sel_hi:[0,1,1]
	v_pk_mul_f32 v[28:29], v[14:15], v[24:25] op_sel:[1,1] op_sel_hi:[0,1] neg_lo:[0,1]
	v_pk_fma_f32 v[24:25], v[14:15], v[24:25], v[28:29] op_sel_hi:[1,0,1]
	v_pk_mul_f32 v[28:29], v[80:81], v[24:25] op_sel:[1,1] op_sel_hi:[1,0] neg_lo:[1,0]
	v_pk_fma_f32 v[28:29], v[80:81], v[24:25], v[28:29] op_sel_hi:[0,1,1]
	ds_write2_b64 v63, v[26:27], v[28:29] offset0:96 offset1:112
	v_pk_mul_f32 v[26:27], v[14:15], v[24:25] op_sel:[1,1] op_sel_hi:[0,1] neg_lo:[0,1]
	v_pk_fma_f32 v[24:25], v[14:15], v[24:25], v[26:27] op_sel_hi:[1,0,1]
	v_pk_mul_f32 v[26:27], v[20:21], v[24:25] op_sel:[1,1] op_sel_hi:[1,0] neg_lo:[1,0]
	v_pk_fma_f32 v[20:21], v[20:21], v[24:25], v[26:27] op_sel_hi:[0,1,1]
	v_pk_mul_f32 v[26:27], v[14:15], v[24:25] op_sel:[1,1] op_sel_hi:[0,1] neg_lo:[0,1]
	v_pk_fma_f32 v[24:25], v[14:15], v[24:25], v[26:27] op_sel_hi:[1,0,1]
	v_pk_mul_f32 v[26:27], v[38:39], v[24:25] op_sel:[1,1] op_sel_hi:[1,0] neg_lo:[1,0]
	v_pk_fma_f32 v[26:27], v[38:39], v[24:25], v[26:27] op_sel_hi:[0,1,1]
	ds_write2_b64 v62, v[20:21], v[26:27] offset0:128 offset1:144
	v_pk_mul_f32 v[20:21], v[14:15], v[24:25] op_sel:[1,1] op_sel_hi:[0,1] neg_lo:[0,1]
	v_pk_fma_f32 v[20:21], v[14:15], v[24:25], v[20:21] op_sel_hi:[1,0,1]
	v_pk_mul_f32 v[24:25], v[22:23], v[20:21] op_sel:[1,1] op_sel_hi:[1,0] neg_lo:[1,0]
	v_pk_fma_f32 v[22:23], v[22:23], v[20:21], v[24:25] op_sel_hi:[0,1,1]
	v_pk_mul_f32 v[24:25], v[14:15], v[20:21] op_sel:[1,1] op_sel_hi:[0,1] neg_lo:[0,1]
	v_pk_fma_f32 v[20:21], v[14:15], v[20:21], v[24:25] op_sel_hi:[1,0,1]
	v_pk_mul_f32 v[24:25], v[42:43], v[20:21] op_sel:[1,1] op_sel_hi:[1,0] neg_lo:[1,0]
	v_pk_fma_f32 v[24:25], v[42:43], v[20:21], v[24:25] op_sel_hi:[0,1,1]
	ds_write2_b64 v61, v[22:23], v[24:25] offset0:160 offset1:176
	v_pk_mul_f32 v[22:23], v[14:15], v[20:21] op_sel:[1,1] op_sel_hi:[0,1] neg_lo:[0,1]
	v_pk_fma_f32 v[20:21], v[14:15], v[20:21], v[22:23] op_sel_hi:[1,0,1]
	v_pk_mul_f32 v[22:23], v[16:17], v[20:21] op_sel:[1,1] op_sel_hi:[1,0] neg_lo:[1,0]
	v_pk_fma_f32 v[16:17], v[16:17], v[20:21], v[22:23] op_sel_hi:[0,1,1]
	v_pk_mul_f32 v[22:23], v[14:15], v[20:21] op_sel:[1,1] op_sel_hi:[0,1] neg_lo:[0,1]
	v_pk_fma_f32 v[20:21], v[14:15], v[20:21], v[22:23] op_sel_hi:[1,0,1]
	v_pk_mul_f32 v[22:23], v[30:31], v[20:21] op_sel:[1,1] op_sel_hi:[1,0] neg_lo:[1,0]
	v_pk_fma_f32 v[22:23], v[30:31], v[20:21], v[22:23] op_sel_hi:[0,1,1]
	ds_write2_b64 v60, v[16:17], v[22:23] offset0:192 offset1:208
	v_pk_mul_f32 v[16:17], v[14:15], v[20:21] op_sel:[1,1] op_sel_hi:[0,1] neg_lo:[0,1]
	v_pk_fma_f32 v[16:17], v[14:15], v[20:21], v[16:17] op_sel_hi:[1,0,1]
	v_pk_mul_f32 v[20:21], v[18:19], v[16:17] op_sel:[1,1] op_sel_hi:[1,0] neg_lo:[1,0]
	v_pk_fma_f32 v[18:19], v[18:19], v[16:17], v[20:21] op_sel_hi:[0,1,1]
	v_pk_mul_f32 v[20:21], v[14:15], v[16:17] op_sel:[1,1] op_sel_hi:[0,1] neg_lo:[0,1]
	v_pk_fma_f32 v[14:15], v[14:15], v[16:17], v[20:21] op_sel_hi:[1,0,1]
	v_pk_mul_f32 v[16:17], v[34:35], v[14:15] op_sel:[1,1] op_sel_hi:[1,0] neg_lo:[1,0]
	v_pk_fma_f32 v[14:15], v[34:35], v[14:15], v[16:17] op_sel_hi:[0,1,1]
	ds_write2_b64 v13, v[18:19], v[14:15] offset0:224 offset1:240
	v_mov_b32_e32 v14, v1
	v_mov_b32_e32 v10, v178
	v_mov_b32_e32 v13, v177
	s_waitcnt lgkmcnt(0)
	s_barrier
	v_mov_b32_e32 v48, v168
	v_xor_b32_e32 v16, 1, v13
	v_lshlrev_b32_e32 v10, 3, v10
	v_lshlrev_b32_e32 v16, 3, v16
	v_add3_u32 v18, 0, v16, v10
	v_xor_b32_e32 v16, 2, v13
	v_lshlrev_b32_e32 v16, 3, v16
	v_xor_b32_e32 v24, 5, v13
	v_add3_u32 v20, 0, v16, v10
	v_xor_b32_e32 v16, 3, v13
	v_lshlrev_b32_e32 v24, 3, v24
	v_lshlrev_b32_e32 v15, 3, v13
	v_lshlrev_b32_e32 v16, 3, v16
	v_add3_u32 v26, 0, v24, v10
	v_xor_b32_e32 v24, 6, v13
	v_add3_u32 v15, 0, v15, v10
	v_add3_u32 v22, 0, v16, v10
	v_lshlrev_b32_e32 v24, 3, v24
	v_xor_b32_e32 v32, 9, v13
	ds_read_b64 v[16:17], v15
	ds_read_b64 v[18:19], v18
	ds_read_b64 v[20:21], v20
	ds_read_b64 v[22:23], v22
	v_xor_b32_e32 v15, 4, v13
	v_add3_u32 v28, 0, v24, v10
	v_xor_b32_e32 v24, 7, v13
	v_lshlrev_b32_e32 v32, 3, v32
	v_lshlrev_b32_e32 v15, 3, v15
	v_lshlrev_b32_e32 v24, 3, v24
	v_add3_u32 v34, 0, v32, v10
	v_xor_b32_e32 v32, 10, v13
	v_add3_u32 v15, 0, v15, v10
	v_add3_u32 v30, 0, v24, v10
	v_lshlrev_b32_e32 v32, 3, v32
	ds_read_b64 v[24:25], v15
	ds_read_b64 v[26:27], v26
	ds_read_b64 v[28:29], v28
	ds_read_b64 v[30:31], v30
	v_xor_b32_e32 v15, 8, v13
	v_add3_u32 v36, 0, v32, v10
	v_xor_b32_e32 v32, 11, v13
	v_lshlrev_b32_e32 v15, 3, v15
	v_lshlrev_b32_e32 v32, 3, v32
	v_xor_b32_e32 v40, 13, v13
	v_add3_u32 v15, 0, v15, v10
	v_add3_u32 v38, 0, v32, v10
	v_lshlrev_b32_e32 v40, 3, v40
	ds_read_b64 v[32:33], v15
	ds_read_b64 v[34:35], v34
	ds_read_b64 v[36:37], v36
	ds_read_b64 v[38:39], v38
	v_xor_b32_e32 v15, 12, v13
	v_add3_u32 v42, 0, v40, v10
	v_xor_b32_e32 v40, 14, v13
	v_xor_b32_e32 v13, 15, v13
	v_lshlrev_b32_e32 v15, 3, v15
	v_lshlrev_b32_e32 v40, 3, v40
	v_lshlrev_b32_e32 v13, 3, v13
	v_add3_u32 v15, 0, v15, v10
	v_add3_u32 v44, 0, v40, v10
	v_add3_u32 v10, 0, v13, v10
	ds_read_b64 v[40:41], v15
	ds_read_b64 v[42:43], v42
	ds_read_b64 v[44:45], v44
	ds_read_b64 v[46:47], v10
	v_mov_b32_e32 v10, v164
	v_mov_b32_e32 v13, v167
	v_mov_b32_e32 v10, v165
	s_waitcnt lgkmcnt(7)
	v_pk_add_f32 v[52:53], v[16:17], v[32:33]
	v_mov_b32_e32 v10, v166
	v_pk_add_f32 v[16:17], v[16:17], v[32:33] neg_lo:[0,1] neg_hi:[0,1]
	s_waitcnt lgkmcnt(6)
	v_pk_add_f32 v[32:33], v[18:19], v[34:35]
	v_pk_add_f32 v[18:19], v[18:19], v[34:35] neg_lo:[0,1] neg_hi:[0,1]
	v_mov_b32_e32 v13, v169
	v_mov_b32_e32 v50, v170
	v_ashrrev_i32_e32 v15, 31, v14
	v_pk_mul_f32 v[34:35], v[18:19], v[50:51] op_sel:[1,0] op_sel_hi:[0,0] neg_lo:[1,1] neg_hi:[0,1]
	v_mov_b32_e32 v13, v171
	v_pk_fma_f32 v[18:19], v[18:19], v[10:11], v[34:35] op_sel_hi:[1,0,1]
	s_waitcnt lgkmcnt(5)
	v_pk_add_f32 v[34:35], v[20:21], v[36:37]
	v_pk_add_f32 v[20:21], v[20:21], v[36:37] neg_lo:[0,1] neg_hi:[0,1]
	s_mov_b32 s39, 0x8000
	v_pk_mul_f32 v[36:37], v[20:21], v[48:49] op_sel:[1,0] op_sel_hi:[0,0] neg_lo:[1,1] neg_hi:[0,1]
	v_mov_b32_e32 v13, v172
	v_pk_fma_f32 v[20:21], v[20:21], v[48:49], v[36:37] op_sel_hi:[1,0,1]
	s_waitcnt lgkmcnt(4)
	v_pk_add_f32 v[36:37], v[22:23], v[38:39]
	v_pk_add_f32 v[22:23], v[22:23], v[38:39] neg_lo:[0,1] neg_hi:[0,1]
	v_pk_mul_f32 v[38:39], v[22:23], v[50:51] op_sel_hi:[1,0]
	v_pk_fma_f32 v[22:23], v[22:23], v[10:11], v[38:39] op_sel:[1,0,0] op_sel_hi:[0,0,1] neg_lo:[1,1,0] neg_hi:[0,1,0]
	s_waitcnt lgkmcnt(3)
	v_pk_add_f32 v[38:39], v[24:25], v[40:41]
	v_pk_add_f32 v[24:25], v[24:25], v[40:41] neg_lo:[0,1] neg_hi:[0,1]
	v_mov_b32_e32 v13, v177
	v_xor_b32_e32 v41, 0x80000000, v24
	v_mov_b32_e32 v40, v25
	s_waitcnt lgkmcnt(2)
	v_pk_add_f32 v[24:25], v[26:27], v[42:43]
	v_pk_add_f32 v[26:27], v[26:27], v[42:43] neg_lo:[0,1] neg_hi:[0,1]
	v_pk_mul_f32 v[42:43], v[26:27], v[50:51] op_sel_hi:[1,0] neg_lo:[0,1] neg_hi:[0,1]
	v_pk_fma_f32 v[26:27], v[26:27], v[10:11], v[42:43] op_sel:[1,0,0] op_sel_hi:[0,0,1] neg_lo:[1,1,0] neg_hi:[0,1,0]
	s_waitcnt lgkmcnt(1)
	v_pk_add_f32 v[42:43], v[28:29], v[44:45]
	v_pk_add_f32 v[28:29], v[28:29], v[44:45] neg_lo:[0,1] neg_hi:[0,1]
	v_pk_mul_f32 v[44:45], v[28:29], v[48:49] op_sel:[1,0] op_sel_hi:[0,0] neg_lo:[1,1] neg_hi:[0,1]
	v_pk_fma_f32 v[28:29], v[28:29], v[48:49], v[44:45] op_sel_hi:[1,0,1] neg_lo:[0,1,0] neg_hi:[0,1,0]
	s_waitcnt lgkmcnt(0)
	v_pk_add_f32 v[44:45], v[30:31], v[46:47]
	v_pk_add_f32 v[30:31], v[30:31], v[46:47] neg_lo:[0,1] neg_hi:[0,1]
	v_pk_mul_f32 v[46:47], v[30:31], v[50:51] op_sel:[1,0] op_sel_hi:[0,0] neg_lo:[1,1] neg_hi:[0,1]
	v_pk_add_f32 v[50:51], v[32:33], v[24:25]
	v_pk_add_f32 v[24:25], v[32:33], v[24:25] neg_lo:[0,1] neg_hi:[0,1]
	v_pk_fma_f32 v[30:31], v[30:31], v[10:11], v[46:47] op_sel_hi:[1,0,1] neg_lo:[0,1,0] neg_hi:[0,1,0]
	v_pk_mul_f32 v[32:33], v[24:25], v[48:49] op_sel:[1,0] op_sel_hi:[0,0] neg_lo:[1,1] neg_hi:[0,1]
	v_pk_add_f32 v[46:47], v[52:53], v[38:39]
	v_pk_fma_f32 v[24:25], v[24:25], v[48:49], v[32:33] op_sel_hi:[1,0,1]
	v_pk_add_f32 v[32:33], v[34:35], v[42:43]
	v_pk_add_f32 v[34:35], v[34:35], v[42:43] neg_lo:[0,1] neg_hi:[0,1]
	v_pk_add_f32 v[38:39], v[52:53], v[38:39] neg_lo:[0,1] neg_hi:[0,1]
	v_xor_b32_e32 v43, 0x80000000, v34
	v_mov_b32_e32 v42, v35
	v_pk_add_f32 v[34:35], v[36:37], v[44:45]
	v_pk_add_f32 v[36:37], v[36:37], v[44:45] neg_lo:[0,1] neg_hi:[0,1]
	v_mov_b32_e32 v10, v179
	v_pk_mul_f32 v[44:45], v[36:37], v[48:49] op_sel:[1,0] op_sel_hi:[0,0] neg_lo:[1,1] neg_hi:[0,1]
	v_pk_fma_f32 v[36:37], v[36:37], v[48:49], v[44:45] op_sel_hi:[1,0,1] neg_lo:[0,1,0] neg_hi:[0,1,0]
	v_pk_add_f32 v[44:45], v[46:47], v[32:33]
	v_pk_add_f32 v[32:33], v[46:47], v[32:33] neg_lo:[0,1] neg_hi:[0,1]
	v_pk_add_f32 v[46:47], v[50:51], v[34:35]
	v_pk_add_f32 v[34:35], v[50:51], v[34:35] neg_lo:[0,1] neg_hi:[0,1]
	v_xor_b32_e32 v51, 0x80000000, v34
	v_mov_b32_e32 v50, v35
	v_pk_add_f32 v[34:35], v[44:45], v[46:47]
	v_pk_add_f32 v[44:45], v[44:45], v[46:47] neg_lo:[0,1] neg_hi:[0,1]
	v_pk_add_f32 v[46:47], v[32:33], v[50:51]
	v_pk_add_f32 v[32:33], v[32:33], v[50:51] neg_lo:[0,1] neg_hi:[0,1]
	v_pk_add_f32 v[50:51], v[38:39], v[42:43]
	v_pk_add_f32 v[38:39], v[38:39], v[42:43] neg_lo:[0,1] neg_hi:[0,1]
	v_pk_add_f32 v[42:43], v[24:25], v[36:37]
	v_pk_add_f32 v[24:25], v[24:25], v[36:37] neg_lo:[0,1] neg_hi:[0,1]
	v_xor_b32_e32 v37, 0x80000000, v24
	v_mov_b32_e32 v36, v25
	v_pk_add_f32 v[24:25], v[50:51], v[42:43]
	v_pk_add_f32 v[42:43], v[50:51], v[42:43] neg_lo:[0,1] neg_hi:[0,1]
	v_pk_add_f32 v[50:51], v[38:39], v[36:37]
	v_pk_add_f32 v[36:37], v[38:39], v[36:37] neg_lo:[0,1] neg_hi:[0,1]
	v_pk_add_f32 v[38:39], v[16:17], v[40:41]
	v_pk_add_f32 v[16:17], v[16:17], v[40:41] neg_lo:[0,1] neg_hi:[0,1]
	v_pk_add_f32 v[40:41], v[18:19], v[26:27]
	v_pk_add_f32 v[18:19], v[18:19], v[26:27] neg_lo:[0,1] neg_hi:[0,1]
	v_pk_mul_f32 v[26:27], v[48:49], v[18:19] op_sel:[0,1] op_sel_hi:[0,0] neg_lo:[1,1] neg_hi:[1,0]
	v_pk_fma_f32 v[18:19], v[48:49], v[18:19], v[26:27] op_sel_hi:[0,1,1]
	v_pk_add_f32 v[26:27], v[20:21], v[28:29]
	v_pk_add_f32 v[20:21], v[20:21], v[28:29] neg_lo:[0,1] neg_hi:[0,1]
	v_xor_b32_e32 v29, 0x80000000, v20
	v_mov_b32_e32 v28, v21
	v_pk_add_f32 v[20:21], v[22:23], v[30:31]
	v_pk_add_f32 v[22:23], v[22:23], v[30:31] neg_lo:[0,1] neg_hi:[0,1]
	v_pk_mul_f32 v[30:31], v[48:49], v[22:23] op_sel:[0,1] op_sel_hi:[0,0] neg_lo:[1,1] neg_hi:[1,0]
	v_pk_fma_f32 v[22:23], v[48:49], v[22:23], v[30:31] op_sel_hi:[0,1,1] neg_lo:[1,0,0] neg_hi:[1,0,0]
	v_pk_add_f32 v[30:31], v[38:39], v[26:27]
	v_pk_add_f32 v[26:27], v[38:39], v[26:27] neg_lo:[0,1] neg_hi:[0,1]
	v_pk_add_f32 v[38:39], v[40:41], v[20:21]
	v_pk_add_f32 v[20:21], v[40:41], v[20:21] neg_lo:[0,1] neg_hi:[0,1]
	v_mov_b32_e32 v48, v168
	v_xor_b32_e32 v41, 0x80000000, v20
	v_mov_b32_e32 v40, v21
	v_pk_add_f32 v[20:21], v[30:31], v[38:39]
	v_pk_add_f32 v[30:31], v[30:31], v[38:39] neg_lo:[0,1] neg_hi:[0,1]
	v_pk_add_f32 v[38:39], v[26:27], v[40:41]
	v_pk_add_f32 v[26:27], v[26:27], v[40:41] neg_lo:[0,1] neg_hi:[0,1]
	v_pk_add_f32 v[40:41], v[16:17], v[28:29]
	v_pk_add_f32 v[16:17], v[16:17], v[28:29] neg_lo:[0,1] neg_hi:[0,1]
	v_pk_add_f32 v[28:29], v[18:19], v[22:23]
	v_pk_add_f32 v[18:19], v[18:19], v[22:23] neg_lo:[0,1] neg_hi:[0,1]
	v_xor_b32_e32 v23, 0x80000000, v18
	v_mov_b32_e32 v22, v19
	v_pk_add_f32 v[18:19], v[40:41], v[28:29]
	v_pk_add_f32 v[28:29], v[40:41], v[28:29] neg_lo:[0,1] neg_hi:[0,1]
	v_pk_add_f32 v[40:41], v[16:17], v[22:23]
	v_pk_add_f32 v[16:17], v[16:17], v[22:23] neg_lo:[0,1] neg_hi:[0,1]
	v_lshl_add_u64 v[22:23], v[14:15], 3, s[48:49]
	global_store_dwordx2 v[22:23], v[34:35], off
	v_add_u32_e32 v22, 0x200, v14
	v_ashrrev_i32_e32 v23, 31, v22
	v_lshl_add_u64 v[22:23], v[22:23], 3, s[48:49]
	global_store_dwordx2 v[22:23], v[20:21], off
	v_add_u32_e32 v20, 0x400, v14
	v_ashrrev_i32_e32 v21, 31, v20
	v_lshl_add_u64 v[20:21], v[20:21], 3, s[48:49]
	global_store_dwordx2 v[20:21], v[24:25], off
	v_add_u32_e32 v20, 0x600, v14
	v_ashrrev_i32_e32 v21, 31, v20
	v_lshl_add_u64 v[20:21], v[20:21], 3, s[48:49]
	global_store_dwordx2 v[20:21], v[18:19], off
	v_add_u32_e32 v18, 0x800, v14
	v_ashrrev_i32_e32 v19, 31, v18
	v_lshl_add_u64 v[18:19], v[18:19], 3, s[48:49]
	global_store_dwordx2 v[18:19], v[46:47], off
	v_add_u32_e32 v18, 0xa00, v14
	v_ashrrev_i32_e32 v19, 31, v18
	v_lshl_add_u64 v[18:19], v[18:19], 3, s[48:49]
	global_store_dwordx2 v[18:19], v[38:39], off
	v_add_u32_e32 v18, 0xc00, v14
	v_ashrrev_i32_e32 v19, 31, v18
	v_lshl_add_u64 v[18:19], v[18:19], 3, s[48:49]
	global_store_dwordx2 v[18:19], v[50:51], off
	v_add_u32_e32 v18, 0xe00, v14
	v_ashrrev_i32_e32 v19, 31, v18
	v_lshl_add_u64 v[18:19], v[18:19], 3, s[48:49]
	global_store_dwordx2 v[18:19], v[40:41], off
	v_add_u32_e32 v18, 0x1000, v14
	v_ashrrev_i32_e32 v19, 31, v18
	v_lshl_add_u64 v[18:19], v[18:19], 3, s[48:49]
	global_store_dwordx2 v[18:19], v[44:45], off
	v_add_u32_e32 v18, 0x1200, v14
	v_ashrrev_i32_e32 v19, 31, v18
	v_lshl_add_u64 v[18:19], v[18:19], 3, s[48:49]
	global_store_dwordx2 v[18:19], v[30:31], off
	v_add_u32_e32 v18, 0x1400, v14
	v_ashrrev_i32_e32 v19, 31, v18
	v_lshl_add_u64 v[18:19], v[18:19], 3, s[48:49]
	global_store_dwordx2 v[18:19], v[42:43], off
	v_add_u32_e32 v18, 0x1600, v14
	v_ashrrev_i32_e32 v19, 31, v18
	v_lshl_add_u64 v[18:19], v[18:19], 3, s[48:49]
	global_store_dwordx2 v[18:19], v[28:29], off
	v_add_u32_e32 v18, 0x1800, v14
	v_ashrrev_i32_e32 v19, 31, v18
	v_lshl_add_u64 v[18:19], v[18:19], 3, s[48:49]
	global_store_dwordx2 v[18:19], v[32:33], off
	v_add_u32_e32 v18, 0x1a00, v14
	v_ashrrev_i32_e32 v19, 31, v18
	v_lshl_add_u64 v[18:19], v[18:19], 3, s[48:49]
	global_store_dwordx2 v[18:19], v[26:27], off
	v_add_u32_e32 v18, 0x1c00, v14
	v_ashrrev_i32_e32 v19, 31, v18
	v_lshl_add_u64 v[18:19], v[18:19], 3, s[48:49]
	global_store_dwordx2 v[18:19], v[36:37], off
	v_add_u32_e32 v18, 0x1e00, v14
	v_ashrrev_i32_e32 v19, 31, v18
	v_lshl_add_u64 v[18:19], v[18:19], 3, s[48:49]
	global_store_dwordx2 v[18:19], v[16:17], off
	v_mov_b32_e32 v50, v170
	v_xor_b32_e32 v16, 1, v13
	v_lshlrev_b32_e32 v10, 3, v10
	v_lshlrev_b32_e32 v16, 3, v16
	v_add3_u32 v18, 0, v16, v10
	v_xor_b32_e32 v16, 2, v13
	v_lshlrev_b32_e32 v16, 3, v16
	v_xor_b32_e32 v24, 5, v13
	v_add3_u32 v20, 0, v16, v10
	v_xor_b32_e32 v16, 3, v13
	v_lshlrev_b32_e32 v24, 3, v24
	v_lshlrev_b32_e32 v15, 3, v13
	v_lshlrev_b32_e32 v16, 3, v16
	v_add3_u32 v26, 0, v24, v10
	v_xor_b32_e32 v24, 6, v13
	v_add3_u32 v15, 0, v15, v10
	v_add3_u32 v22, 0, v16, v10
	v_lshlrev_b32_e32 v24, 3, v24
	v_xor_b32_e32 v32, 9, v13
	ds_read_b64 v[16:17], v15
	ds_read_b64 v[18:19], v18
	ds_read_b64 v[20:21], v20
	ds_read_b64 v[22:23], v22
	v_xor_b32_e32 v15, 4, v13
	v_add3_u32 v28, 0, v24, v10
	v_xor_b32_e32 v24, 7, v13
	v_lshlrev_b32_e32 v32, 3, v32
	v_lshlrev_b32_e32 v15, 3, v15
	v_lshlrev_b32_e32 v24, 3, v24
	v_add3_u32 v34, 0, v32, v10
	v_xor_b32_e32 v32, 10, v13
	v_add3_u32 v15, 0, v15, v10
	v_add3_u32 v30, 0, v24, v10
	v_lshlrev_b32_e32 v32, 3, v32
	ds_read_b64 v[24:25], v15
	ds_read_b64 v[26:27], v26
	ds_read_b64 v[28:29], v28
	ds_read_b64 v[30:31], v30
	v_xor_b32_e32 v15, 8, v13
	v_add3_u32 v36, 0, v32, v10
	v_xor_b32_e32 v32, 11, v13
	v_lshlrev_b32_e32 v15, 3, v15
	v_lshlrev_b32_e32 v32, 3, v32
	v_xor_b32_e32 v40, 13, v13
	v_add3_u32 v15, 0, v15, v10
	v_add3_u32 v38, 0, v32, v10
	v_lshlrev_b32_e32 v40, 3, v40
	ds_read_b64 v[32:33], v15
	ds_read_b64 v[34:35], v34
	ds_read_b64 v[36:37], v36
	ds_read_b64 v[38:39], v38
	v_xor_b32_e32 v15, 12, v13
	v_add3_u32 v42, 0, v40, v10
	v_xor_b32_e32 v40, 14, v13
	v_xor_b32_e32 v13, 15, v13
	v_lshlrev_b32_e32 v15, 3, v15
	v_lshlrev_b32_e32 v40, 3, v40
	v_lshlrev_b32_e32 v13, 3, v13
	v_add3_u32 v15, 0, v15, v10
	v_add3_u32 v44, 0, v40, v10
	v_add3_u32 v10, 0, v13, v10
	ds_read_b64 v[40:41], v15
	ds_read_b64 v[42:43], v42
	ds_read_b64 v[44:45], v44
	ds_read_b64 v[46:47], v10
	v_mov_b32_e32 v10, v164
	v_mov_b32_e32 v13, v167
	v_mov_b32_e32 v10, v165
	s_waitcnt lgkmcnt(7)
	v_pk_add_f32 v[52:53], v[16:17], v[32:33]
	v_mov_b32_e32 v10, v166
	v_pk_add_f32 v[16:17], v[16:17], v[32:33] neg_lo:[0,1] neg_hi:[0,1]
	s_waitcnt lgkmcnt(6)
	v_pk_add_f32 v[32:33], v[18:19], v[34:35]
	v_pk_add_f32 v[18:19], v[18:19], v[34:35] neg_lo:[0,1] neg_hi:[0,1]
	v_mov_b32_e32 v13, v169
	s_nop 0
	v_pk_mul_f32 v[34:35], v[18:19], v[50:51] op_sel:[1,0] op_sel_hi:[0,0] neg_lo:[1,1] neg_hi:[0,1]
	v_mov_b32_e32 v13, v171
	v_pk_fma_f32 v[18:19], v[18:19], v[10:11], v[34:35] op_sel_hi:[1,0,1]
	s_waitcnt lgkmcnt(5)
	v_pk_add_f32 v[34:35], v[20:21], v[36:37]
	v_pk_add_f32 v[20:21], v[20:21], v[36:37] neg_lo:[0,1] neg_hi:[0,1]
	v_pk_mul_f32 v[36:37], v[20:21], v[48:49] op_sel:[1,0] op_sel_hi:[0,0] neg_lo:[1,1] neg_hi:[0,1]
	v_mov_b32_e32 v13, v172
	v_pk_fma_f32 v[20:21], v[20:21], v[48:49], v[36:37] op_sel_hi:[1,0,1]
	s_waitcnt lgkmcnt(4)
	v_pk_add_f32 v[36:37], v[22:23], v[38:39]
	v_pk_add_f32 v[22:23], v[22:23], v[38:39] neg_lo:[0,1] neg_hi:[0,1]
	v_pk_mul_f32 v[38:39], v[22:23], v[50:51] op_sel_hi:[1,0]
	v_pk_fma_f32 v[22:23], v[22:23], v[10:11], v[38:39] op_sel:[1,0,0] op_sel_hi:[0,0,1] neg_lo:[1,1,0] neg_hi:[0,1,0]
	s_waitcnt lgkmcnt(3)
	v_pk_add_f32 v[38:39], v[24:25], v[40:41]
	v_pk_add_f32 v[24:25], v[24:25], v[40:41] neg_lo:[0,1] neg_hi:[0,1]
	v_mov_b32_e32 v13, v174
	v_xor_b32_e32 v41, 0x80000000, v24
	v_mov_b32_e32 v40, v25
	s_waitcnt lgkmcnt(2)
	v_pk_add_f32 v[24:25], v[26:27], v[42:43]
	v_pk_add_f32 v[26:27], v[26:27], v[42:43] neg_lo:[0,1] neg_hi:[0,1]
	v_pk_mul_f32 v[42:43], v[26:27], v[50:51] op_sel_hi:[1,0] neg_lo:[0,1] neg_hi:[0,1]
	v_pk_fma_f32 v[26:27], v[26:27], v[10:11], v[42:43] op_sel:[1,0,0] op_sel_hi:[0,0,1] neg_lo:[1,1,0] neg_hi:[0,1,0]
	s_waitcnt lgkmcnt(1)
	v_pk_add_f32 v[42:43], v[28:29], v[44:45]
	v_pk_add_f32 v[28:29], v[28:29], v[44:45] neg_lo:[0,1] neg_hi:[0,1]
	v_pk_mul_f32 v[44:45], v[28:29], v[48:49] op_sel:[1,0] op_sel_hi:[0,0] neg_lo:[1,1] neg_hi:[0,1]
	v_pk_fma_f32 v[28:29], v[28:29], v[48:49], v[44:45] op_sel_hi:[1,0,1] neg_lo:[0,1,0] neg_hi:[0,1,0]
	s_waitcnt lgkmcnt(0)
	v_pk_add_f32 v[44:45], v[30:31], v[46:47]
	v_pk_add_f32 v[30:31], v[30:31], v[46:47] neg_lo:[0,1] neg_hi:[0,1]
	v_pk_mul_f32 v[46:47], v[30:31], v[50:51] op_sel:[1,0] op_sel_hi:[0,0] neg_lo:[1,1] neg_hi:[0,1]
	v_pk_add_f32 v[50:51], v[32:33], v[24:25]
	v_pk_add_f32 v[24:25], v[32:33], v[24:25] neg_lo:[0,1] neg_hi:[0,1]
	v_pk_fma_f32 v[30:31], v[30:31], v[10:11], v[46:47] op_sel_hi:[1,0,1] neg_lo:[0,1,0] neg_hi:[0,1,0]
	v_pk_mul_f32 v[32:33], v[24:25], v[48:49] op_sel:[1,0] op_sel_hi:[0,0] neg_lo:[1,1] neg_hi:[0,1]
	v_pk_add_f32 v[46:47], v[52:53], v[38:39]
	v_pk_fma_f32 v[24:25], v[24:25], v[48:49], v[32:33] op_sel_hi:[1,0,1]
	v_pk_add_f32 v[32:33], v[34:35], v[42:43]
	v_pk_add_f32 v[34:35], v[34:35], v[42:43] neg_lo:[0,1] neg_hi:[0,1]
	v_pk_add_f32 v[38:39], v[52:53], v[38:39] neg_lo:[0,1] neg_hi:[0,1]
	v_xor_b32_e32 v43, 0x80000000, v34
	v_mov_b32_e32 v42, v35
	v_pk_add_f32 v[34:35], v[36:37], v[44:45]
	v_pk_add_f32 v[36:37], v[36:37], v[44:45] neg_lo:[0,1] neg_hi:[0,1]
	v_mov_b32_e32 v10, v184
	v_pk_mul_f32 v[44:45], v[36:37], v[48:49] op_sel:[1,0] op_sel_hi:[0,0] neg_lo:[1,1] neg_hi:[0,1]
	v_pk_fma_f32 v[36:37], v[36:37], v[48:49], v[44:45] op_sel_hi:[1,0,1] neg_lo:[0,1,0] neg_hi:[0,1,0]
	v_pk_add_f32 v[44:45], v[46:47], v[32:33]
	v_pk_add_f32 v[32:33], v[46:47], v[32:33] neg_lo:[0,1] neg_hi:[0,1]
	v_pk_add_f32 v[46:47], v[50:51], v[34:35]
	v_pk_add_f32 v[34:35], v[50:51], v[34:35] neg_lo:[0,1] neg_hi:[0,1]
	v_xor_b32_e32 v51, 0x80000000, v34
	v_mov_b32_e32 v50, v35
	v_pk_add_f32 v[34:35], v[44:45], v[46:47]
	v_pk_add_f32 v[44:45], v[44:45], v[46:47] neg_lo:[0,1] neg_hi:[0,1]
	v_pk_add_f32 v[46:47], v[32:33], v[50:51]
	v_pk_add_f32 v[32:33], v[32:33], v[50:51] neg_lo:[0,1] neg_hi:[0,1]
	v_pk_add_f32 v[50:51], v[38:39], v[42:43]
	v_pk_add_f32 v[38:39], v[38:39], v[42:43] neg_lo:[0,1] neg_hi:[0,1]
	v_pk_add_f32 v[42:43], v[24:25], v[36:37]
	v_pk_add_f32 v[24:25], v[24:25], v[36:37] neg_lo:[0,1] neg_hi:[0,1]
	v_xor_b32_e32 v37, 0x80000000, v24
	v_mov_b32_e32 v36, v25
	v_pk_add_f32 v[24:25], v[50:51], v[42:43]
	v_pk_add_f32 v[42:43], v[50:51], v[42:43] neg_lo:[0,1] neg_hi:[0,1]
	v_pk_add_f32 v[50:51], v[38:39], v[36:37]
	v_pk_add_f32 v[36:37], v[38:39], v[36:37] neg_lo:[0,1] neg_hi:[0,1]
	v_pk_add_f32 v[38:39], v[16:17], v[40:41]
	v_pk_add_f32 v[16:17], v[16:17], v[40:41] neg_lo:[0,1] neg_hi:[0,1]
	v_pk_add_f32 v[40:41], v[18:19], v[26:27]
	v_pk_add_f32 v[18:19], v[18:19], v[26:27] neg_lo:[0,1] neg_hi:[0,1]
	v_pk_mul_f32 v[26:27], v[48:49], v[18:19] op_sel:[0,1] op_sel_hi:[0,0] neg_lo:[1,1] neg_hi:[1,0]
	v_pk_fma_f32 v[18:19], v[48:49], v[18:19], v[26:27] op_sel_hi:[0,1,1]
	v_pk_add_f32 v[26:27], v[20:21], v[28:29]
	v_pk_add_f32 v[20:21], v[20:21], v[28:29] neg_lo:[0,1] neg_hi:[0,1]
	v_xor_b32_e32 v29, 0x80000000, v20
	v_mov_b32_e32 v28, v21
	v_pk_add_f32 v[20:21], v[22:23], v[30:31]
	v_pk_add_f32 v[22:23], v[22:23], v[30:31] neg_lo:[0,1] neg_hi:[0,1]
	v_pk_mul_f32 v[30:31], v[48:49], v[22:23] op_sel:[0,1] op_sel_hi:[0,0] neg_lo:[1,1] neg_hi:[1,0]
	v_pk_fma_f32 v[22:23], v[48:49], v[22:23], v[30:31] op_sel_hi:[0,1,1] neg_lo:[1,0,0] neg_hi:[1,0,0]
	v_pk_add_f32 v[30:31], v[38:39], v[26:27]
	v_pk_add_f32 v[26:27], v[38:39], v[26:27] neg_lo:[0,1] neg_hi:[0,1]
	v_pk_add_f32 v[38:39], v[40:41], v[20:21]
	v_pk_add_f32 v[20:21], v[40:41], v[20:21] neg_lo:[0,1] neg_hi:[0,1]
	v_xor_b32_e32 v41, 0x80000000, v20
	v_mov_b32_e32 v40, v21
	v_pk_add_f32 v[20:21], v[30:31], v[38:39]
	v_pk_add_f32 v[30:31], v[30:31], v[38:39] neg_lo:[0,1] neg_hi:[0,1]
	v_pk_add_f32 v[38:39], v[26:27], v[40:41]
	v_pk_add_f32 v[26:27], v[26:27], v[40:41] neg_lo:[0,1] neg_hi:[0,1]
	v_pk_add_f32 v[40:41], v[16:17], v[28:29]
	v_pk_add_f32 v[16:17], v[16:17], v[28:29] neg_lo:[0,1] neg_hi:[0,1]
	v_pk_add_f32 v[28:29], v[18:19], v[22:23]
	v_pk_add_f32 v[18:19], v[18:19], v[22:23] neg_lo:[0,1] neg_hi:[0,1]
	v_xor_b32_e32 v23, 0x80000000, v18
	v_mov_b32_e32 v22, v19
	v_pk_add_f32 v[18:19], v[40:41], v[28:29]
	v_pk_add_f32 v[28:29], v[40:41], v[28:29] neg_lo:[0,1] neg_hi:[0,1]
	v_pk_add_f32 v[40:41], v[16:17], v[22:23]
	v_pk_add_f32 v[16:17], v[16:17], v[22:23] neg_lo:[0,1] neg_hi:[0,1]
	v_add_u32_e32 v22, 0x2000, v14
	v_ashrrev_i32_e32 v23, 31, v22
	v_lshl_add_u64 v[22:23], v[22:23], 3, s[48:49]
	global_store_dwordx2 v[22:23], v[34:35], off
	v_add_u32_e32 v22, 0x2200, v14
	v_ashrrev_i32_e32 v23, 31, v22
	v_lshl_add_u64 v[22:23], v[22:23], 3, s[48:49]
	global_store_dwordx2 v[22:23], v[20:21], off
	v_add_u32_e32 v20, 0x2400, v14
	v_ashrrev_i32_e32 v21, 31, v20
	v_lshl_add_u64 v[20:21], v[20:21], 3, s[48:49]
	global_store_dwordx2 v[20:21], v[24:25], off
	v_add_u32_e32 v20, 0x2600, v14
	v_ashrrev_i32_e32 v21, 31, v20
	v_lshl_add_u64 v[20:21], v[20:21], 3, s[48:49]
	global_store_dwordx2 v[20:21], v[18:19], off
	v_add_u32_e32 v18, 0x2800, v14
	v_ashrrev_i32_e32 v19, 31, v18
	v_lshl_add_u64 v[18:19], v[18:19], 3, s[48:49]
	global_store_dwordx2 v[18:19], v[46:47], off
	v_add_u32_e32 v18, 0x2a00, v14
	v_ashrrev_i32_e32 v19, 31, v18
	v_lshl_add_u64 v[18:19], v[18:19], 3, s[48:49]
	global_store_dwordx2 v[18:19], v[38:39], off
	v_add_u32_e32 v18, 0x2c00, v14
	v_ashrrev_i32_e32 v19, 31, v18
	v_lshl_add_u64 v[18:19], v[18:19], 3, s[48:49]
	global_store_dwordx2 v[18:19], v[50:51], off
	v_add_u32_e32 v18, 0x2e00, v14
	v_ashrrev_i32_e32 v19, 31, v18
	v_lshl_add_u64 v[18:19], v[18:19], 3, s[48:49]
	global_store_dwordx2 v[18:19], v[40:41], off
	v_add_u32_e32 v18, 0x3000, v14
	v_ashrrev_i32_e32 v19, 31, v18
	v_lshl_add_u64 v[18:19], v[18:19], 3, s[48:49]
	global_store_dwordx2 v[18:19], v[44:45], off
	v_add_u32_e32 v18, 0x3200, v14
	v_ashrrev_i32_e32 v19, 31, v18
	v_lshl_add_u64 v[18:19], v[18:19], 3, s[48:49]
	global_store_dwordx2 v[18:19], v[30:31], off
	v_add_u32_e32 v18, 0x3400, v14
	v_ashrrev_i32_e32 v19, 31, v18
	v_lshl_add_u64 v[18:19], v[18:19], 3, s[48:49]
	global_store_dwordx2 v[18:19], v[42:43], off
	v_add_u32_e32 v18, 0x3600, v14
	v_ashrrev_i32_e32 v19, 31, v18
	v_lshl_add_u64 v[18:19], v[18:19], 3, s[48:49]
	global_store_dwordx2 v[18:19], v[28:29], off
	v_add_u32_e32 v18, 0x3800, v14
	v_ashrrev_i32_e32 v19, 31, v18
	v_lshl_add_u64 v[18:19], v[18:19], 3, s[48:49]
	global_store_dwordx2 v[18:19], v[32:33], off
	v_add_u32_e32 v18, 0x3a00, v14
	v_ashrrev_i32_e32 v19, 31, v18
	v_lshl_add_u64 v[18:19], v[18:19], 3, s[48:49]
	global_store_dwordx2 v[18:19], v[26:27], off
	v_add_u32_e32 v18, 0x3c00, v14
	v_add_u32_e32 v14, 0x3e00, v14
	v_ashrrev_i32_e32 v15, 31, v14
	v_ashrrev_i32_e32 v19, 31, v18
	v_lshl_add_u64 v[14:15], v[14:15], 3, s[48:49]
	v_lshl_add_u64 v[18:19], v[18:19], 3, s[48:49]
	global_store_dwordx2 v[14:15], v[16:17], off
	v_mov_b32_e32 v16, v185
	v_mov_b32_e32 v14, v1
	global_store_dwordx2 v[18:19], v[36:37], off
	s_barrier
	s_nop 0
	v_pk_mul_f32 v[36:37], v[16:17], s[66:67] op_sel_hi:[0,1] neg_lo:[1,0]
	s_mov_b64 s[66:67], vcc
	v_ashrrev_i32_e32 v15, 31, v14
	v_lshl_add_u64 v[18:19], v[14:15], 2, s[66:67]
	v_add_co_u32_e32 v28, vcc, s85, v18
	v_pk_mul_f32 v[52:53], v[16:17], s[60:61] op_sel_hi:[0,1] neg_lo:[1,0]
	s_nop 0
	v_addc_co_u32_e32 v29, vcc, 0, v19, vcc
	v_add_co_u32_e32 v20, vcc, s84, v18
	s_movk_i32 s61, 0x3000
	s_nop 0
	v_addc_co_u32_e32 v21, vcc, 0, v19, vcc
	v_add_co_u32_e32 v48, vcc, s61, v18
	v_pk_mul_f32 v[54:55], v[16:17], s[94:95] op_sel_hi:[0,1] neg_lo:[1,0]
	s_nop 0
	v_addc_co_u32_e32 v49, vcc, 0, v19, vcc
	v_add_co_u32_e32 v22, vcc, s45, v18
	v_pk_mul_f32 v[82:83], v[16:17], s[68:69] op_sel_hi:[0,1] neg_lo:[1,0]
	s_nop 0
	v_addc_co_u32_e32 v23, vcc, 0, v19, vcc
	v_add_co_u32_e32 v58, vcc, s86, v18
	s_mov_b32 s68, 0x3f7ec46d
	s_nop 0
	v_addc_co_u32_e32 v59, vcc, 0, v19, vcc
	v_add_co_u32_e32 v60, vcc, s88, v18
	v_pk_mul_f32 v[32:33], v[16:17], s[78:79] op_sel_hi:[0,1] neg_lo:[1,0]
	s_nop 0
	v_addc_co_u32_e32 v61, vcc, 0, v19, vcc
	v_add_co_u32_e32 v66, vcc, s90, v18
	v_pk_mul_f32 v[40:41], v[16:17], s[80:81] op_sel_hi:[0,1] neg_lo:[1,0]
	s_nop 0
	v_addc_co_u32_e32 v67, vcc, 0, v19, vcc
	v_add_co_u32_e32 v68, vcc, s39, v18
	s_mov_b32 s39, 0x9000
	s_nop 0
	v_addc_co_u32_e32 v69, vcc, 0, v19, vcc
	v_add_co_u32_e32 v24, vcc, s39, v18
	s_mov_b32 s39, 0xb000
	s_nop 0
	v_addc_co_u32_e32 v25, vcc, 0, v19, vcc
	v_add_co_u32_e32 v26, vcc, s91, v18
	s_mov_b32 s80, 0x3f54db31
	s_nop 0
	v_addc_co_u32_e32 v27, vcc, 0, v19, vcc
	v_add_co_u32_e32 v34, vcc, s39, v18
	s_mov_b32 s39, 0xc000
	s_nop 0
	v_addc_co_u32_e32 v35, vcc, 0, v19, vcc
	v_add_co_u32_e32 v38, vcc, s39, v18
	s_mov_b32 s39, 0xd000
	s_nop 0
	v_addc_co_u32_e32 v39, vcc, 0, v19, vcc
	v_add_co_u32_e32 v46, vcc, s39, v18
	s_mov_b32 s39, 0xe000
	s_nop 0
	v_addc_co_u32_e32 v47, vcc, 0, v19, vcc
	v_add_co_u32_e32 v50, vcc, s39, v18
	s_mov_b32 s39, 0xf000
	s_nop 0
	v_addc_co_u32_e32 v51, vcc, 0, v19, vcc
	v_add_co_u32_e32 v70, vcc, s39, v18
	s_mov_b32 s69, 0xbdc8bd36
	s_nop 0
	v_addc_co_u32_e32 v71, vcc, 0, v19, vcc
	global_load_dword v90, v[68:69], off
	global_load_dword v92, v[68:69], off offset:2048
	global_load_dword v94, v[26:27], off offset:-4096
	global_load_dword v96, v[24:25], off offset:2048
	global_load_dword v98, v[26:27], off
	global_load_dword v100, v[26:27], off offset:2048
	global_load_dword v102, v[38:39], off offset:-4096
	global_load_dword v104, v[34:35], off offset:2048
	global_load_dword v106, v[38:39], off
	global_load_dword v108, v[38:39], off offset:2048
	global_load_dword v110, v[50:51], off offset:-4096
	global_load_dword v112, v[46:47], off offset:2048
	global_load_dword v114, v[50:51], off
	global_load_dword v116, v[50:51], off offset:2048
	global_load_dword v118, v[70:71], off
	global_load_dword v56, v[20:21], off
	s_nop 0
	global_load_dword v50, v[20:21], off offset:2048
	global_load_dword v120, v[70:71], off offset:2048
	global_load_dword v46, v[22:23], off offset:-4096
	global_load_dword v38, v[22:23], off
	global_load_dword v74, v[20:21], off offset:-4096
	global_load_dword v34, v[22:23], off offset:2048
	global_load_dword v26, v[60:61], off offset:-4096
	global_load_dword v24, v[60:61], off
	s_nop 0
	global_load_dword v22, v[60:61], off offset:2048
	global_load_dword v20, v[68:69], off offset:-4096
	s_nop 0
	global_load_dword v68, v[18:19], off
	global_load_dword v76, v[18:19], off offset:2048
	global_load_dword v72, v[28:29], off offset:2048
	s_nop 0
	global_load_dword v48, v[48:49], off offset:2048
	s_nop 0
	global_load_dword v28, v[58:59], off offset:2048
	global_load_dword v18, v[66:67], off offset:2048
	s_mov_b32 s88, 0x3e47c5c2
	v_pk_fma_f32 v[58:59], v[10:11], s[74:75], v[54:55] op_sel_hi:[0,1,1]
	s_mov_b32 s74, 0x3f226799
	s_mov_b32 s81, 0xbf0e39da
	v_pk_mul_f32 v[42:43], v[16:17], s[52:53] op_sel_hi:[0,1] neg_lo:[1,0]
	v_pk_mul_f32 v[64:65], v[16:17], s[62:63] op_sel_hi:[0,1] neg_lo:[1,0]
	s_mov_b32 s89, 0xbf7b14be
	v_pk_fma_f32 v[124:125], v[10:11], s[68:69], v[32:33] op_sel_hi:[0,1,1]
	s_mov_b32 s75, 0xbf45e403
	s_mov_b32 s52, 0x3f3504f3
	v_pk_mul_f32 v[32:33], v[16:17], s[30:31] op_sel_hi:[0,1] neg_lo:[1,0]
	s_mov_b32 s30, 0x3dc8bd36
	v_pk_mul_f32 v[62:63], v[16:17], s[56:57] op_sel_hi:[0,1] neg_lo:[1,0]
	v_pk_fma_f32 v[60:61], v[10:11], s[80:81], v[52:53] op_sel_hi:[0,1,1]
	s_mov_b32 s53, 0xbf3504f3
	v_pk_fma_f32 v[52:53], v[10:11], s[74:75], v[64:65] op_sel_hi:[0,1,1]
	s_mov_b32 s31, 0xbf7ec46d
	v_pk_fma_f32 v[64:65], v[10:11], s[88:89], v[32:33] op_sel_hi:[0,1,1]
	v_pk_mul_f32 v[32:33], v[16:17], s[34:35] op_sel_hi:[0,1] neg_lo:[1,0]
	s_mov_b32 s78, 0x3f61c598
	v_pk_fma_f32 v[54:55], v[10:11], s[52:53], v[62:63] op_sel_hi:[0,1,1]
	v_pk_fma_f32 v[62:63], v[10:11], s[30:31], v[32:33] op_sel_hi:[0,1,1]
	v_pk_mul_f32 v[32:33], v[16:17], s[36:37] op_sel_hi:[0,1] neg_lo:[1,0]
	s_mov_b32 s79, 0xbef15aea
	v_pk_mul_f32 v[44:45], v[16:17], s[50:51] op_sel_hi:[0,1] neg_lo:[1,0]
	v_pk_fma_f32 v[32:33], v[10:11], s[76:77], v[32:33] op_sel_hi:[0,1,1]
	s_mov_b32 s94, 0x3f6c835e
	v_pk_fma_f32 v[66:67], v[10:11], s[78:79], v[44:45] op_sel_hi:[0,1,1]
	v_pk_fma_f32 v[44:45], v[10:11], s[82:83], v[82:83] op_sel_hi:[0,1,1]
	s_mov_b32 s82, 0x3ef15aea
	s_mov_b32 s95, 0xbec3ef15
	v_pk_mul_f32 v[84:85], v[16:17], s[70:71] op_sel_hi:[0,1] neg_lo:[1,0]
	s_mov_b32 s83, 0xbf61c598
	v_pk_mul_f32 v[30:31], v[16:17], s[40:41] op_sel_hi:[0,1] neg_lo:[1,0]
	s_mov_b32 s84, 0x3ec3ef15
	s_mov_b32 s40, 0x3f74fa0b
	v_pk_fma_f32 v[70:71], v[10:11], s[94:95], v[42:43] op_sel_hi:[0,1,1]
	v_pk_fma_f32 v[42:43], v[10:11], s[82:83], v[84:85] op_sel_hi:[0,1,1]
	s_mov_b32 s85, 0xbf6c835e
	s_mov_b32 s41, 0xbe94a031
	v_pk_mul_f32 v[86:87], v[16:17], s[58:59] op_sel_hi:[0,1] neg_lo:[1,0]
	s_mov_b32 s86, 0x3e94a031
	v_pk_fma_f32 v[78:79], v[10:11], s[40:41], v[40:41] op_sel_hi:[0,1,1]
	v_pk_fma_f32 v[40:41], v[10:11], s[84:85], v[86:87] op_sel_hi:[0,1,1]
	s_mov_b32 s87, 0xbf74fa0b
	v_pk_mul_f32 v[88:89], v[16:17], s[64:65] op_sel_hi:[0,1] neg_lo:[1,0]
	v_pk_fma_f32 v[122:123], v[10:11], s[46:47], v[30:31] op_sel_hi:[0,1,1]
	v_pk_fma_f32 v[30:31], v[10:11], s[86:87], v[88:89] op_sel_hi:[0,1,1]
	s_waitcnt vmcnt(31)
	v_pk_mul_f32 v[82:83], v[32:33], v[90:91] op_sel_hi:[1,0]
	v_pk_mul_f32 v[32:33], v[16:17], s[2:3] op_sel_hi:[0,1] neg_lo:[1,0]
	v_pk_fma_f32 v[32:33], v[10:11], s[0:1], v[32:33] op_sel_hi:[0,1,1]
	s_waitcnt vmcnt(30)
	v_pk_mul_f32 v[84:85], v[32:33], v[92:93] op_sel_hi:[1,0]
	v_pk_mul_f32 v[32:33], v[16:17], s[6:7] op_sel_hi:[0,1] neg_lo:[1,0]
	v_pk_fma_f32 v[32:33], v[10:11], s[4:5], v[32:33] op_sel_hi:[0,1,1]
	s_waitcnt vmcnt(29)
	v_pk_mul_f32 v[86:87], v[32:33], v[94:95] op_sel_hi:[1,0]
	v_pk_mul_f32 v[32:33], v[16:17], s[10:11] op_sel_hi:[0,1] neg_lo:[1,0]
	v_pk_fma_f32 v[32:33], v[10:11], s[8:9], v[32:33] op_sel_hi:[0,1,1]
	s_waitcnt vmcnt(28)
	v_pk_mul_f32 v[88:89], v[32:33], v[96:97] op_sel_hi:[1,0]
	v_pk_mul_f32 v[32:33], v[16:17], s[16:17] op_sel_hi:[0,1] neg_lo:[1,0]
	v_pk_fma_f32 v[32:33], v[10:11], s[12:13], v[32:33] op_sel_hi:[0,1,1]
	s_waitcnt vmcnt(27)
	v_pk_mul_f32 v[90:91], v[32:33], v[98:99] op_sel_hi:[1,0]
	v_pk_mul_f32 v[32:33], v[16:17], s[20:21] op_sel_hi:[0,1] neg_lo:[1,0]
	v_pk_fma_f32 v[32:33], v[10:11], s[18:19], v[32:33] op_sel_hi:[0,1,1]
	s_waitcnt vmcnt(26)
	v_pk_mul_f32 v[92:93], v[32:33], v[100:101] op_sel_hi:[1,0]
	v_pk_mul_f32 v[32:33], v[16:17], s[24:25] op_sel_hi:[0,1] neg_lo:[1,0]
	v_pk_fma_f32 v[32:33], v[10:11], s[22:23], v[32:33] op_sel_hi:[0,1,1]
	s_waitcnt vmcnt(25)
	v_pk_mul_f32 v[94:95], v[32:33], v[102:103] op_sel_hi:[1,0]
	v_pk_mul_f32 v[32:33], v[16:17], s[28:29] op_sel_hi:[0,1] neg_lo:[1,0]
	v_pk_fma_f32 v[32:33], v[10:11], s[26:27], v[32:33] op_sel_hi:[0,1,1]
	s_waitcnt vmcnt(24)
	v_pk_mul_f32 v[96:97], v[32:33], v[104:105] op_sel_hi:[1,0]
	v_pk_mul_f32 v[32:33], v[16:17], s[52:53] op_sel_hi:[0,0] neg_lo:[1,0]
	v_pk_fma_f32 v[32:33], v[10:11], s[38:39], v[32:33] op_sel_hi:[0,0,1] neg_lo:[0,0,1] neg_hi:[0,0,1]
	s_waitcnt vmcnt(23)
	v_pk_mul_f32 v[98:99], v[32:33], v[106:107] op_sel_hi:[1,0]
	v_pk_mul_f32 v[32:33], v[16:17], s[26:27] op_sel_hi:[0,1] neg_lo:[1,0]
	v_pk_fma_f32 v[32:33], v[10:11], s[28:29], v[32:33] op_sel_hi:[0,1,1]
	s_waitcnt vmcnt(22)
	v_pk_mul_f32 v[100:101], v[32:33], v[108:109] op_sel_hi:[1,0]
	v_pk_mul_f32 v[32:33], v[16:17], s[22:23] op_sel_hi:[0,1] neg_lo:[1,0]
	v_pk_fma_f32 v[32:33], v[10:11], s[24:25], v[32:33] op_sel_hi:[0,1,1]
	s_waitcnt vmcnt(21)
	v_pk_mul_f32 v[102:103], v[32:33], v[110:111] op_sel_hi:[1,0]
	v_pk_mul_f32 v[32:33], v[16:17], s[18:19] op_sel_hi:[0,1] neg_lo:[1,0]
	v_pk_fma_f32 v[32:33], v[10:11], s[20:21], v[32:33] op_sel_hi:[0,1,1]
	s_waitcnt vmcnt(20)
	v_pk_mul_f32 v[104:105], v[32:33], v[112:113] op_sel_hi:[1,0]
	v_pk_mul_f32 v[32:33], v[16:17], s[12:13] op_sel_hi:[0,1] neg_lo:[1,0]
	v_pk_fma_f32 v[32:33], v[10:11], s[16:17], v[32:33] op_sel_hi:[0,1,1]
	s_waitcnt vmcnt(19)
	v_pk_mul_f32 v[106:107], v[32:33], v[114:115] op_sel_hi:[1,0]
	v_pk_mul_f32 v[32:33], v[16:17], s[8:9] op_sel_hi:[0,1] neg_lo:[1,0]
	v_pk_fma_f32 v[32:33], v[10:11], s[10:11], v[32:33] op_sel_hi:[0,1,1]
	s_mov_b32 s70, 0x3f7b14be
	s_waitcnt vmcnt(18)
	v_pk_mul_f32 v[108:109], v[32:33], v[116:117] op_sel_hi:[1,0]
	v_pk_mul_f32 v[32:33], v[16:17], s[4:5] op_sel_hi:[0,1] neg_lo:[1,0]
	v_pk_mul_f32 v[16:17], v[16:17], s[0:1] op_sel_hi:[0,1] neg_lo:[1,0]
	s_mov_b32 s71, 0xbe47c5c2
	v_pk_fma_f32 v[16:17], v[10:11], s[2:3], v[16:17] op_sel_hi:[0,1,1]
	v_pk_fma_f32 v[80:81], v[10:11], s[70:71], v[36:37] op_sel_hi:[0,1,1]
	v_pk_fma_f32 v[32:33], v[10:11], s[6:7], v[32:33] op_sel_hi:[0,1,1]
	s_waitcnt vmcnt(14)
	v_pk_mul_f32 v[112:113], v[16:17], v[120:121] op_sel_hi:[1,0]
	v_mov_b32_e32 v10, v164
	s_waitcnt vmcnt(5)
	v_pk_fma_f32 v[126:127], v[68:69], v[122:123], v[82:83] op_sel_hi:[0,1,1]
	v_pk_fma_f32 v[68:69], v[68:69], v[122:123], v[82:83] op_sel_hi:[0,1,1] neg_lo:[0,0,1] neg_hi:[0,0,1]
	s_waitcnt vmcnt(4)
	v_pk_fma_f32 v[82:83], v[124:125], v[76:77], v[84:85] op_sel_hi:[1,0,1]
	v_pk_fma_f32 v[76:77], v[124:125], v[76:77], v[84:85] op_sel_hi:[1,0,1] neg_lo:[0,0,1] neg_hi:[0,0,1]
	v_pk_mul_f32 v[110:111], v[32:33], v[118:119] op_sel_hi:[1,0]
	v_mov_b32_e32 v114, v165
	v_mov_b32_e32 v32, v166
	v_mov_b32_e32 v116, v167
	v_mov_b32_e32 v10, v168
	v_mov_b32_e32 v118, v169
	v_mov_b32_e32 v36, v170
	v_mov_b32_e32 v120, v171
	v_mov_b32_e32 v15, v172
	v_pk_mul_f32 v[84:85], v[76:77], v[120:121] op_sel:[1,0] op_sel_hi:[0,0] neg_lo:[1,1] neg_hi:[0,1]
	v_pk_fma_f32 v[76:77], v[76:77], v[114:115], v[84:85] op_sel_hi:[1,0,1]
	v_pk_fma_f32 v[84:85], v[80:81], v[74:75], v[86:87] op_sel_hi:[1,0,1]
	v_pk_fma_f32 v[74:75], v[80:81], v[74:75], v[86:87] op_sel_hi:[1,0,1] neg_lo:[0,0,1] neg_hi:[0,0,1]
	v_pk_mul_f32 v[80:81], v[74:75], v[36:37] op_sel:[1,0] op_sel_hi:[0,0] neg_lo:[1,1] neg_hi:[0,1]
	v_pk_fma_f32 v[74:75], v[74:75], v[32:33], v[80:81] op_sel_hi:[1,0,1]
	s_waitcnt vmcnt(3)
	v_pk_fma_f32 v[80:81], v[78:79], v[72:73], v[88:89] op_sel_hi:[1,0,1]
	v_pk_fma_f32 v[72:73], v[78:79], v[72:73], v[88:89] op_sel_hi:[1,0,1] neg_lo:[0,0,1] neg_hi:[0,0,1]
	v_pk_mul_f32 v[78:79], v[72:73], v[118:119] op_sel:[1,0] op_sel_hi:[0,0] neg_lo:[1,1] neg_hi:[0,1]
	v_pk_fma_f32 v[72:73], v[72:73], v[116:117], v[78:79] op_sel_hi:[1,0,1]
	v_pk_fma_f32 v[78:79], v[70:71], v[56:57], v[90:91] op_sel_hi:[1,0,1]
	v_pk_fma_f32 v[56:57], v[70:71], v[56:57], v[90:91] op_sel_hi:[1,0,1] neg_lo:[0,0,1] neg_hi:[0,0,1]
	v_pk_mul_f32 v[70:71], v[56:57], v[10:11] op_sel:[1,0] op_sel_hi:[0,0] neg_lo:[1,1] neg_hi:[0,1]
	v_pk_fma_f32 v[56:57], v[56:57], v[10:11], v[70:71] op_sel_hi:[1,0,1]
	v_pk_fma_f32 v[70:71], v[66:67], v[50:51], v[92:93] op_sel_hi:[1,0,1]
	v_pk_fma_f32 v[50:51], v[66:67], v[50:51], v[92:93] op_sel_hi:[1,0,1] neg_lo:[0,0,1] neg_hi:[0,0,1]
	v_pk_mul_f32 v[66:67], v[50:51], v[118:119] op_sel_hi:[1,0]
	v_xor_b32_e32 v86, 0x80000000, v51
	v_mov_b32_e32 v87, v50
	v_pk_fma_f32 v[50:51], v[60:61], v[46:47], v[94:95] op_sel_hi:[1,0,1]
	v_pk_fma_f32 v[46:47], v[60:61], v[46:47], v[94:95] op_sel_hi:[1,0,1] neg_lo:[0,0,1] neg_hi:[0,0,1]
	v_pk_fma_f32 v[66:67], v[86:87], v[116:117], v[66:67] op_sel_hi:[1,0,1] neg_lo:[0,1,0] neg_hi:[0,1,0]
	v_pk_mul_f32 v[60:61], v[46:47], v[36:37] op_sel_hi:[1,0]
	v_xor_b32_e32 v86, 0x80000000, v47
	v_mov_b32_e32 v87, v46
	s_waitcnt vmcnt(2)
	v_pk_fma_f32 v[46:47], v[58:59], v[48:49], v[96:97] op_sel_hi:[1,0,1]
	v_pk_fma_f32 v[48:49], v[58:59], v[48:49], v[96:97] op_sel_hi:[1,0,1] neg_lo:[0,0,1] neg_hi:[0,0,1]
	v_pk_fma_f32 v[60:61], v[86:87], v[32:33], v[60:61] op_sel_hi:[1,0,1] neg_lo:[0,1,0] neg_hi:[0,1,0]
	v_pk_mul_f32 v[58:59], v[48:49], v[120:121] op_sel_hi:[1,0]
	v_pk_fma_f32 v[48:49], v[48:49], v[114:115], v[58:59] op_sel:[1,0,0] op_sel_hi:[0,0,1] neg_lo:[1,1,0] neg_hi:[0,1,0]
	v_pk_fma_f32 v[58:59], v[54:55], v[38:39], v[98:99] op_sel_hi:[1,0,1]
	v_pk_fma_f32 v[38:39], v[54:55], v[38:39], v[98:99] op_sel_hi:[1,0,1] neg_lo:[0,0,1] neg_hi:[0,0,1]
	v_xor_b32_e32 v55, 0x80000000, v38
	v_mov_b32_e32 v54, v39
	v_pk_fma_f32 v[38:39], v[52:53], v[34:35], v[100:101] op_sel_hi:[1,0,1]
	v_pk_fma_f32 v[34:35], v[52:53], v[34:35], v[100:101] op_sel_hi:[1,0,1] neg_lo:[0,0,1] neg_hi:[0,0,1]
	v_pk_mul_f32 v[52:53], v[34:35], v[120:121] op_sel_hi:[1,0] neg_lo:[0,1] neg_hi:[0,1]
	v_xor_b32_e32 v86, 0x80000000, v35
	v_mov_b32_e32 v87, v34
	v_pk_fma_f32 v[34:35], v[44:45], v[26:27], v[102:103] op_sel_hi:[1,0,1]
	v_pk_fma_f32 v[26:27], v[44:45], v[26:27], v[102:103] op_sel_hi:[1,0,1] neg_lo:[0,0,1] neg_hi:[0,0,1]
	v_pk_fma_f32 v[52:53], v[86:87], v[114:115], v[52:53] op_sel_hi:[1,0,1] neg_lo:[0,1,0] neg_hi:[0,1,0]
	v_pk_mul_f32 v[44:45], v[26:27], v[36:37] op_sel_hi:[1,0] neg_lo:[0,1] neg_hi:[0,1]
	v_xor_b32_e32 v86, 0x80000000, v27
	v_mov_b32_e32 v87, v26
	s_waitcnt vmcnt(1)
	v_pk_fma_f32 v[26:27], v[42:43], v[28:29], v[104:105] op_sel_hi:[1,0,1]
	v_pk_fma_f32 v[28:29], v[42:43], v[28:29], v[104:105] op_sel_hi:[1,0,1] neg_lo:[0,0,1] neg_hi:[0,0,1]
	v_pk_fma_f32 v[86:87], v[86:87], v[32:33], v[44:45] op_sel_hi:[1,0,1] neg_lo:[0,1,0] neg_hi:[0,1,0]
	v_pk_mul_f32 v[42:43], v[28:29], v[118:119] op_sel_hi:[1,0] neg_lo:[0,1] neg_hi:[0,1]
	v_xor_b32_e32 v44, 0x80000000, v29
	v_mov_b32_e32 v45, v28
	v_pk_fma_f32 v[28:29], v[40:41], v[24:25], v[106:107] op_sel_hi:[1,0,1]
	v_pk_fma_f32 v[24:25], v[40:41], v[24:25], v[106:107] op_sel_hi:[1,0,1] neg_lo:[0,0,1] neg_hi:[0,0,1]
	v_pk_fma_f32 v[42:43], v[44:45], v[116:117], v[42:43] op_sel_hi:[1,0,1] neg_lo:[0,1,0] neg_hi:[0,1,0]
	v_pk_mul_f32 v[40:41], v[24:25], v[10:11] op_sel:[1,0] op_sel_hi:[0,0] neg_lo:[1,1] neg_hi:[0,1]
	v_pk_add_f32 v[44:45], v[126:127], v[58:59] neg_lo:[0,1] neg_hi:[0,1]
	v_pk_fma_f32 v[88:89], v[24:25], v[10:11], v[40:41] op_sel_hi:[1,0,1] neg_lo:[0,1,0] neg_hi:[0,1,0]
	v_pk_fma_f32 v[24:25], v[30:31], v[22:23], v[108:109] op_sel_hi:[1,0,1]
	v_pk_fma_f32 v[22:23], v[30:31], v[22:23], v[108:109] op_sel_hi:[1,0,1] neg_lo:[0,0,1] neg_hi:[0,0,1]
	v_pk_mul_f32 v[30:31], v[22:23], v[118:119] op_sel:[1,0] op_sel_hi:[0,0] neg_lo:[1,1] neg_hi:[0,1]
	v_pk_fma_f32 v[90:91], v[22:23], v[116:117], v[30:31] op_sel_hi:[1,0,1] neg_lo:[0,1,0] neg_hi:[0,1,0]
	v_pk_fma_f32 v[22:23], v[64:65], v[20:21], v[110:111] op_sel_hi:[1,0,1]
	v_pk_fma_f32 v[20:21], v[64:65], v[20:21], v[110:111] op_sel_hi:[1,0,1] neg_lo:[0,0,1] neg_hi:[0,0,1]
	v_pk_mul_f32 v[30:31], v[20:21], v[36:37] op_sel:[1,0] op_sel_hi:[0,0] neg_lo:[1,1] neg_hi:[0,1]
	v_pk_fma_f32 v[64:65], v[20:21], v[32:33], v[30:31] op_sel_hi:[1,0,1] neg_lo:[0,1,0] neg_hi:[0,1,0]
	s_waitcnt vmcnt(0)
	v_pk_fma_f32 v[20:21], v[62:63], v[18:19], v[112:113] op_sel_hi:[1,0,1]
	v_pk_fma_f32 v[18:19], v[62:63], v[18:19], v[112:113] op_sel_hi:[1,0,1] neg_lo:[0,0,1] neg_hi:[0,0,1]
	v_pk_mul_f32 v[30:31], v[18:19], v[120:121] op_sel:[1,0] op_sel_hi:[0,0] neg_lo:[1,1] neg_hi:[0,1]
	v_pk_fma_f32 v[62:63], v[18:19], v[114:115], v[30:31] op_sel_hi:[1,0,1] neg_lo:[0,1,0] neg_hi:[0,1,0]
	v_pk_add_f32 v[30:31], v[82:83], v[38:39]
	v_pk_add_f32 v[38:39], v[82:83], v[38:39] neg_lo:[0,1] neg_hi:[0,1]
	v_pk_add_f32 v[18:19], v[126:127], v[58:59]
	v_pk_mul_f32 v[40:41], v[38:39], v[36:37] op_sel:[1,0] op_sel_hi:[0,0] neg_lo:[1,1] neg_hi:[0,1]
	v_pk_fma_f32 v[38:39], v[38:39], v[32:33], v[40:41] op_sel_hi:[1,0,1]
	v_pk_add_f32 v[40:41], v[84:85], v[34:35]
	v_pk_add_f32 v[34:35], v[84:85], v[34:35] neg_lo:[0,1] neg_hi:[0,1]
	v_pk_mul_f32 v[58:59], v[34:35], v[10:11] op_sel:[1,0] op_sel_hi:[0,0] neg_lo:[1,1] neg_hi:[0,1]
	v_pk_fma_f32 v[34:35], v[34:35], v[10:11], v[58:59] op_sel_hi:[1,0,1]
	v_pk_add_f32 v[58:59], v[80:81], v[26:27]
	v_pk_add_f32 v[26:27], v[80:81], v[26:27] neg_lo:[0,1] neg_hi:[0,1]
	v_pk_mul_f32 v[80:81], v[26:27], v[36:37] op_sel_hi:[1,0]
	v_xor_b32_e32 v82, 0x80000000, v27
	v_mov_b32_e32 v83, v26
	v_pk_add_f32 v[26:27], v[78:79], v[28:29]
	v_pk_add_f32 v[28:29], v[78:79], v[28:29] neg_lo:[0,1] neg_hi:[0,1]
	v_pk_fma_f32 v[80:81], v[82:83], v[32:33], v[80:81] op_sel_hi:[1,0,1] neg_lo:[0,1,0] neg_hi:[0,1,0]
	v_xor_b32_e32 v79, 0x80000000, v28
	v_mov_b32_e32 v78, v29
	v_pk_add_f32 v[28:29], v[70:71], v[24:25]
	v_pk_add_f32 v[24:25], v[70:71], v[24:25] neg_lo:[0,1] neg_hi:[0,1]
	v_pk_mul_f32 v[70:71], v[24:25], v[36:37] op_sel_hi:[1,0] neg_lo:[0,1] neg_hi:[0,1]
	v_pk_fma_f32 v[24:25], v[24:25], v[32:33], v[70:71] op_sel:[1,0,0] op_sel_hi:[0,0,1] neg_lo:[1,1,0] neg_hi:[0,1,0]
	v_pk_add_f32 v[70:71], v[50:51], v[22:23]
	v_pk_add_f32 v[22:23], v[50:51], v[22:23] neg_lo:[0,1] neg_hi:[0,1]
	v_pk_mul_f32 v[50:51], v[22:23], v[10:11] op_sel:[1,0] op_sel_hi:[0,0] neg_lo:[1,1] neg_hi:[0,1]
	v_pk_fma_f32 v[50:51], v[22:23], v[10:11], v[50:51] op_sel_hi:[1,0,1] neg_lo:[0,1,0] neg_hi:[0,1,0]
	v_pk_add_f32 v[22:23], v[46:47], v[20:21]
	v_pk_add_f32 v[20:21], v[46:47], v[20:21] neg_lo:[0,1] neg_hi:[0,1]
	v_pk_mul_f32 v[46:47], v[20:21], v[36:37] op_sel:[1,0] op_sel_hi:[0,0] neg_lo:[1,1] neg_hi:[0,1]
	v_pk_fma_f32 v[20:21], v[20:21], v[32:33], v[46:47] op_sel_hi:[1,0,1] neg_lo:[0,1,0] neg_hi:[0,1,0]
	v_pk_add_f32 v[46:47], v[18:19], v[26:27]
	v_pk_add_f32 v[18:19], v[18:19], v[26:27] neg_lo:[0,1] neg_hi:[0,1]
	v_pk_add_f32 v[26:27], v[30:31], v[28:29]
	v_pk_add_f32 v[28:29], v[30:31], v[28:29] neg_lo:[0,1] neg_hi:[0,1]
	v_pk_mul_f32 v[30:31], v[28:29], v[10:11] op_sel:[1,0] op_sel_hi:[0,0] neg_lo:[1,1] neg_hi:[0,1]
	v_pk_fma_f32 v[28:29], v[28:29], v[10:11], v[30:31] op_sel_hi:[1,0,1]
	v_pk_add_f32 v[30:31], v[40:41], v[70:71]
	v_pk_add_f32 v[40:41], v[40:41], v[70:71] neg_lo:[0,1] neg_hi:[0,1]
	v_pk_add_f32 v[82:83], v[46:47], v[30:31] neg_lo:[0,1] neg_hi:[0,1]
	v_xor_b32_e32 v71, 0x80000000, v40
	v_mov_b32_e32 v70, v41
	v_pk_add_f32 v[40:41], v[58:59], v[22:23]
	v_pk_add_f32 v[22:23], v[58:59], v[22:23] neg_lo:[0,1] neg_hi:[0,1]
	v_pk_mul_f32 v[58:59], v[22:23], v[10:11] op_sel:[1,0] op_sel_hi:[0,0] neg_lo:[1,1] neg_hi:[0,1]
	v_pk_fma_f32 v[58:59], v[22:23], v[10:11], v[58:59] op_sel_hi:[1,0,1] neg_lo:[0,1,0] neg_hi:[0,1,0]
	v_pk_add_f32 v[22:23], v[46:47], v[30:31]
	v_pk_add_f32 v[30:31], v[26:27], v[40:41]
	v_pk_add_f32 v[26:27], v[26:27], v[40:41] neg_lo:[0,1] neg_hi:[0,1]
	v_pk_add_f32 v[84:85], v[22:23], v[30:31]
	v_pk_add_f32 v[30:31], v[22:23], v[30:31] neg_lo:[0,1] neg_hi:[0,1]
	v_pk_add_f32 v[46:47], v[82:83], v[26:27] op_sel:[0,1] op_sel_hi:[1,0] neg_hi:[0,1]
	v_pk_add_f32 v[22:23], v[82:83], v[26:27] op_sel:[0,1] op_sel_hi:[1,0] neg_lo:[0,1]
	v_pk_add_f32 v[40:41], v[28:29], v[58:59]
	v_pk_add_f32 v[28:29], v[28:29], v[58:59] neg_lo:[0,1] neg_hi:[0,1]
	v_pk_add_f32 v[26:27], v[18:19], v[70:71]
	v_pk_add_f32 v[18:19], v[18:19], v[70:71] neg_lo:[0,1] neg_hi:[0,1]
	v_pk_add_f32 v[70:71], v[26:27], v[40:41]
	v_pk_add_f32 v[26:27], v[26:27], v[40:41] neg_lo:[0,1] neg_hi:[0,1]
	v_pk_add_f32 v[40:41], v[18:19], v[28:29] op_sel:[0,1] op_sel_hi:[1,0] neg_hi:[0,1]
	v_pk_add_f32 v[18:19], v[18:19], v[28:29] op_sel:[0,1] op_sel_hi:[1,0] neg_lo:[0,1]
	v_pk_add_f32 v[58:59], v[38:39], v[24:25]
	v_pk_add_f32 v[24:25], v[38:39], v[24:25] neg_lo:[0,1] neg_hi:[0,1]
	v_pk_add_f32 v[28:29], v[44:45], v[78:79]
	v_pk_mul_f32 v[38:39], v[10:11], v[24:25] op_sel:[0,1] op_sel_hi:[0,0] neg_lo:[1,1] neg_hi:[1,0]
	v_pk_fma_f32 v[38:39], v[10:11], v[24:25], v[38:39] op_sel_hi:[0,1,1]
	v_pk_add_f32 v[24:25], v[34:35], v[50:51]
	v_pk_add_f32 v[34:35], v[34:35], v[50:51] neg_lo:[0,1] neg_hi:[0,1]
	v_pk_add_f32 v[44:45], v[44:45], v[78:79] neg_lo:[0,1] neg_hi:[0,1]
	v_xor_b32_e32 v79, 0x80000000, v34
	v_mov_b32_e32 v78, v35
	v_pk_add_f32 v[34:35], v[80:81], v[20:21]
	v_pk_add_f32 v[20:21], v[80:81], v[20:21] neg_lo:[0,1] neg_hi:[0,1]
	v_pk_mul_f32 v[50:51], v[10:11], v[20:21] op_sel:[0,1] op_sel_hi:[0,0] neg_lo:[1,1] neg_hi:[1,0]
	v_pk_fma_f32 v[20:21], v[10:11], v[20:21], v[50:51] op_sel_hi:[0,1,1] neg_lo:[1,0,0] neg_hi:[1,0,0]
	v_pk_add_f32 v[50:51], v[28:29], v[24:25]
	v_pk_add_f32 v[24:25], v[28:29], v[24:25] neg_lo:[0,1] neg_hi:[0,1]
	v_pk_add_f32 v[28:29], v[58:59], v[34:35]
	v_pk_add_f32 v[34:35], v[58:59], v[34:35] neg_lo:[0,1] neg_hi:[0,1]
	v_pk_add_f32 v[80:81], v[50:51], v[28:29]
	v_xor_b32_e32 v59, 0x80000000, v34
	v_mov_b32_e32 v58, v35
	v_pk_add_f32 v[34:35], v[50:51], v[28:29] neg_lo:[0,1] neg_hi:[0,1]
	v_pk_add_f32 v[50:51], v[24:25], v[58:59]
	v_pk_add_f32 v[24:25], v[24:25], v[58:59] neg_lo:[0,1] neg_hi:[0,1]
	v_pk_add_f32 v[28:29], v[44:45], v[78:79]
	v_pk_add_f32 v[58:59], v[44:45], v[78:79] neg_lo:[0,1] neg_hi:[0,1]
	v_pk_add_f32 v[44:45], v[38:39], v[20:21]
	v_pk_add_f32 v[20:21], v[38:39], v[20:21] neg_lo:[0,1] neg_hi:[0,1]
	v_pk_add_f32 v[78:79], v[28:29], v[44:45]
	v_pk_add_f32 v[28:29], v[28:29], v[44:45] neg_lo:[0,1] neg_hi:[0,1]
	v_pk_add_f32 v[44:45], v[58:59], v[20:21] op_sel:[0,1] op_sel_hi:[1,0] neg_hi:[0,1]
	v_pk_add_f32 v[20:21], v[58:59], v[20:21] op_sel:[0,1] op_sel_hi:[1,0] neg_lo:[0,1]
	v_pk_add_f32 v[38:39], v[68:69], v[54:55]
	v_pk_add_f32 v[58:59], v[68:69], v[54:55] neg_lo:[0,1] neg_hi:[0,1]
	v_pk_add_f32 v[54:55], v[76:77], v[52:53]
	v_pk_add_f32 v[52:53], v[76:77], v[52:53] neg_lo:[0,1] neg_hi:[0,1]
	v_pk_mul_f32 v[68:69], v[36:37], v[52:53] op_sel:[0,1] op_sel_hi:[0,0] neg_lo:[1,1] neg_hi:[1,0]
	v_pk_fma_f32 v[52:53], v[32:33], v[52:53], v[68:69] op_sel_hi:[0,1,1]
	v_pk_add_f32 v[68:69], v[74:75], v[86:87]
	v_pk_add_f32 v[74:75], v[74:75], v[86:87] neg_lo:[0,1] neg_hi:[0,1]
	v_pk_mul_f32 v[76:77], v[10:11], v[74:75] op_sel:[0,1] op_sel_hi:[0,0] neg_lo:[1,1] neg_hi:[1,0]
	v_pk_fma_f32 v[74:75], v[10:11], v[74:75], v[76:77] op_sel_hi:[0,1,1]
	v_pk_add_f32 v[76:77], v[72:73], v[42:43]
	v_pk_add_f32 v[42:43], v[72:73], v[42:43] neg_lo:[0,1] neg_hi:[0,1]
	v_pk_mul_f32 v[72:73], v[32:33], v[42:43] op_sel:[0,1] op_sel_hi:[0,0] neg_lo:[1,1] neg_hi:[1,0]
	v_pk_fma_f32 v[42:43], v[36:37], v[42:43], v[72:73] op_sel_hi:[0,1,1]
	v_pk_add_f32 v[72:73], v[56:57], v[88:89]
	v_pk_add_f32 v[56:57], v[56:57], v[88:89] neg_lo:[0,1] neg_hi:[0,1]
	v_xor_b32_e32 v83, 0x80000000, v56
	v_mov_b32_e32 v82, v57
	v_pk_add_f32 v[56:57], v[66:67], v[90:91]
	v_pk_add_f32 v[66:67], v[66:67], v[90:91] neg_lo:[0,1] neg_hi:[0,1]
	v_pk_mul_f32 v[86:87], v[32:33], v[66:67] op_sel:[0,1] op_sel_hi:[0,0] neg_lo:[1,1] neg_hi:[1,0]
	v_pk_fma_f32 v[66:67], v[36:37], v[66:67], v[86:87] op_sel_hi:[0,1,1] neg_lo:[1,0,0] neg_hi:[1,0,0]
	v_pk_add_f32 v[86:87], v[60:61], v[64:65]
	v_pk_add_f32 v[60:61], v[60:61], v[64:65] neg_lo:[0,1] neg_hi:[0,1]
	v_pk_mul_f32 v[64:65], v[10:11], v[60:61] op_sel:[0,1] op_sel_hi:[0,0] neg_lo:[1,1] neg_hi:[1,0]
	v_pk_fma_f32 v[60:61], v[10:11], v[60:61], v[64:65] op_sel_hi:[0,1,1] neg_lo:[1,0,0] neg_hi:[1,0,0]
	v_pk_add_f32 v[64:65], v[48:49], v[62:63]
	v_pk_add_f32 v[48:49], v[48:49], v[62:63] neg_lo:[0,1] neg_hi:[0,1]
	v_pk_mul_f32 v[36:37], v[36:37], v[48:49] op_sel:[0,1] op_sel_hi:[0,0] neg_lo:[1,1] neg_hi:[1,0]
	v_pk_fma_f32 v[36:37], v[32:33], v[48:49], v[36:37] op_sel_hi:[0,1,1] neg_lo:[1,0,0] neg_hi:[1,0,0]
	v_pk_add_f32 v[32:33], v[38:39], v[72:73]
	v_pk_add_f32 v[48:49], v[38:39], v[72:73] neg_lo:[0,1] neg_hi:[0,1]
	v_pk_add_f32 v[38:39], v[56:57], v[54:55]
	v_pk_add_f32 v[54:55], v[54:55], v[56:57] neg_lo:[0,1] neg_hi:[0,1]
	v_pk_add_f32 v[62:63], v[68:69], v[86:87] neg_lo:[0,1] neg_hi:[0,1]
	v_pk_mul_f32 v[56:57], v[10:11], v[54:55] op_sel:[0,1] op_sel_hi:[0,0] neg_lo:[1,1] neg_hi:[1,0]
	v_pk_fma_f32 v[56:57], v[10:11], v[54:55], v[56:57] op_sel_hi:[0,1,1]
	v_pk_add_f32 v[54:55], v[68:69], v[86:87]
	v_xor_b32_e32 v69, 0x80000000, v62
	v_mov_b32_e32 v68, v63
	v_pk_add_f32 v[62:63], v[76:77], v[64:65]
	v_pk_add_f32 v[64:65], v[76:77], v[64:65] neg_lo:[0,1] neg_hi:[0,1]
	v_pk_mul_f32 v[72:73], v[10:11], v[64:65] op_sel:[0,1] op_sel_hi:[0,0] neg_lo:[1,1] neg_hi:[1,0]
	v_pk_fma_f32 v[64:65], v[10:11], v[64:65], v[72:73] op_sel_hi:[0,1,1] neg_lo:[1,0,0] neg_hi:[1,0,0]
	v_pk_add_f32 v[72:73], v[32:33], v[54:55]
	v_pk_add_f32 v[32:33], v[32:33], v[54:55] neg_lo:[0,1] neg_hi:[0,1]
	v_pk_add_f32 v[54:55], v[38:39], v[62:63]
	v_pk_add_f32 v[38:39], v[38:39], v[62:63] neg_lo:[0,1] neg_hi:[0,1]
	v_pk_add_f32 v[76:77], v[72:73], v[54:55]
	v_pk_add_f32 v[54:55], v[72:73], v[54:55] neg_lo:[0,1] neg_hi:[0,1]
	v_pk_add_f32 v[72:73], v[32:33], v[38:39] op_sel:[0,1] op_sel_hi:[1,0] neg_hi:[0,1]
	v_pk_add_f32 v[38:39], v[32:33], v[38:39] op_sel:[0,1] op_sel_hi:[1,0] neg_lo:[0,1]
	v_pk_add_f32 v[32:33], v[48:49], v[68:69]
	v_pk_add_f32 v[62:63], v[48:49], v[68:69] neg_lo:[0,1] neg_hi:[0,1]
	v_pk_add_f32 v[48:49], v[56:57], v[64:65]
	v_pk_add_f32 v[56:57], v[56:57], v[64:65] neg_lo:[0,1] neg_hi:[0,1]
	v_xor_b32_e32 v65, 0x80000000, v56
	v_mov_b32_e32 v64, v57
	v_pk_add_f32 v[56:57], v[32:33], v[48:49]
	v_pk_add_f32 v[48:49], v[32:33], v[48:49] neg_lo:[0,1] neg_hi:[0,1]
	v_pk_add_f32 v[68:69], v[62:63], v[64:65]
	v_pk_add_f32 v[32:33], v[62:63], v[64:65] neg_lo:[0,1] neg_hi:[0,1]
	v_pk_add_f32 v[64:65], v[66:67], v[52:53]
	v_pk_add_f32 v[52:53], v[52:53], v[66:67] neg_lo:[0,1] neg_hi:[0,1]
	v_pk_add_f32 v[62:63], v[58:59], v[82:83]
	v_pk_mul_f32 v[66:67], v[10:11], v[52:53] op_sel:[0,1] op_sel_hi:[0,0] neg_lo:[1,1] neg_hi:[1,0]
	v_pk_fma_f32 v[52:53], v[10:11], v[52:53], v[66:67] op_sel_hi:[0,1,1]
	v_pk_add_f32 v[66:67], v[74:75], v[60:61]
	v_pk_add_f32 v[60:61], v[74:75], v[60:61] neg_lo:[0,1] neg_hi:[0,1]
	v_pk_add_f32 v[58:59], v[58:59], v[82:83] neg_lo:[0,1] neg_hi:[0,1]
	v_xor_b32_e32 v75, 0x80000000, v60
	v_mov_b32_e32 v74, v61
	v_pk_add_f32 v[60:61], v[42:43], v[36:37]
	v_pk_add_f32 v[36:37], v[42:43], v[36:37] neg_lo:[0,1] neg_hi:[0,1]
	v_pk_mul_f32 v[42:43], v[10:11], v[36:37] op_sel:[0,1] op_sel_hi:[0,0] neg_lo:[1,1] neg_hi:[1,0]
	v_pk_fma_f32 v[36:37], v[10:11], v[36:37], v[42:43] op_sel_hi:[0,1,1] neg_lo:[1,0,0] neg_hi:[1,0,0]
	v_pk_add_f32 v[42:43], v[62:63], v[66:67]
	v_pk_add_f32 v[62:63], v[62:63], v[66:67] neg_lo:[0,1] neg_hi:[0,1]
	v_pk_add_f32 v[66:67], v[64:65], v[60:61]
	v_pk_add_f32 v[60:61], v[64:65], v[60:61] neg_lo:[0,1] neg_hi:[0,1]
	v_lshl_add_u32 v10, v13, 3, 0
	v_xor_b32_e32 v65, 0x80000000, v60
	v_mov_b32_e32 v64, v61
	v_pk_add_f32 v[60:61], v[42:43], v[66:67]
	v_pk_add_f32 v[66:67], v[42:43], v[66:67] neg_lo:[0,1] neg_hi:[0,1]
	v_pk_add_f32 v[82:83], v[62:63], v[64:65]
	v_pk_add_f32 v[42:43], v[62:63], v[64:65] neg_lo:[0,1] neg_hi:[0,1]
	v_pk_add_f32 v[64:65], v[52:53], v[36:37]
	v_pk_add_f32 v[36:37], v[52:53], v[36:37] neg_lo:[0,1] neg_hi:[0,1]
	v_pk_add_f32 v[62:63], v[58:59], v[74:75]
	v_pk_add_f32 v[58:59], v[58:59], v[74:75] neg_lo:[0,1] neg_hi:[0,1]
	v_pk_add_f32 v[86:87], v[62:63], v[64:65]
	v_pk_add_f32 v[52:53], v[62:63], v[64:65] neg_lo:[0,1] neg_hi:[0,1]
	v_pk_add_f32 v[62:63], v[58:59], v[36:37] op_sel:[0,1] op_sel_hi:[1,0] neg_hi:[0,1]
	v_pk_add_f32 v[36:37], v[58:59], v[36:37] op_sel:[0,1] op_sel_hi:[1,0] neg_lo:[0,1]
	v_pk_mul_f32 v[58:59], v[84:85], s[14:15] op_sel:[1,0] neg_lo:[1,0]
	v_pk_fma_f32 v[58:59], v[84:85], s[42:43], v[58:59] op_sel_hi:[0,1,1]
	ds_write_b64 v10, v[58:59]
	v_pk_fma_f32 v[58:59], v[180:181], s[92:93], v[180:181] op_sel:[1,0,0] op_sel_hi:[0,1,1]
	v_pk_mul_f32 v[64:65], v[58:59], v[76:77] op_sel:[1,1] op_sel_hi:[0,1] neg_lo:[0,1]
	v_pk_fma_f32 v[64:65], v[58:59], v[76:77], v[64:65] op_sel_hi:[1,0,1]
	ds_write_b64 v10, v[64:65] offset:4224
	v_pk_mul_f32 v[64:65], v[180:181], v[58:59] op_sel:[1,1] op_sel_hi:[0,1] neg_lo:[0,1]
	v_pk_fma_f32 v[58:59], v[180:181], v[58:59], v[64:65] op_sel_hi:[1,0,1]
	v_pk_mul_f32 v[64:65], v[58:59], v[80:81] op_sel:[1,1] op_sel_hi:[0,1] neg_lo:[0,1]
	v_pk_fma_f32 v[64:65], v[58:59], v[80:81], v[64:65] op_sel_hi:[1,0,1]
	ds_write_b64 v10, v[64:65] offset:8448
	v_pk_mul_f32 v[64:65], v[180:181], v[58:59] op_sel:[1,1] op_sel_hi:[0,1] neg_lo:[0,1]
	v_pk_fma_f32 v[58:59], v[180:181], v[58:59], v[64:65] op_sel_hi:[1,0,1]
	v_pk_mul_f32 v[64:65], v[58:59], v[60:61] op_sel:[1,1] op_sel_hi:[0,1] neg_lo:[0,1]
	v_pk_fma_f32 v[60:61], v[58:59], v[60:61], v[64:65] op_sel_hi:[1,0,1]
	ds_write_b64 v10, v[60:61] offset:12672
	v_pk_mul_f32 v[60:61], v[180:181], v[58:59] op_sel:[1,1] op_sel_hi:[0,1] neg_lo:[0,1]
	v_pk_fma_f32 v[58:59], v[180:181], v[58:59], v[60:61] op_sel_hi:[1,0,1]
	v_pk_mul_f32 v[60:61], v[70:71], v[58:59] op_sel:[1,1] op_sel_hi:[1,0] neg_lo:[1,0]
	v_pk_fma_f32 v[60:61], v[70:71], v[58:59], v[60:61] op_sel_hi:[0,1,1]
	ds_write_b64 v10, v[60:61] offset:16896
	v_pk_mul_f32 v[60:61], v[180:181], v[58:59] op_sel:[1,1] op_sel_hi:[0,1] neg_lo:[0,1]
	v_pk_fma_f32 v[58:59], v[180:181], v[58:59], v[60:61] op_sel_hi:[1,0,1]
	v_pk_mul_f32 v[60:61], v[58:59], v[56:57] op_sel:[1,1] op_sel_hi:[0,1] neg_lo:[0,1]
	v_pk_fma_f32 v[56:57], v[58:59], v[56:57], v[60:61] op_sel_hi:[1,0,1]
	ds_write_b64 v10, v[56:57] offset:21120
	v_pk_mul_f32 v[56:57], v[180:181], v[58:59] op_sel:[1,1] op_sel_hi:[0,1] neg_lo:[0,1]
	v_pk_fma_f32 v[56:57], v[180:181], v[58:59], v[56:57] op_sel_hi:[1,0,1]
	v_pk_mul_f32 v[58:59], v[78:79], v[56:57] op_sel:[1,1] op_sel_hi:[1,0] neg_lo:[1,0]
	v_pk_fma_f32 v[58:59], v[78:79], v[56:57], v[58:59] op_sel_hi:[0,1,1]
	ds_write_b64 v10, v[58:59] offset:25344
	v_pk_mul_f32 v[58:59], v[180:181], v[56:57] op_sel:[1,1] op_sel_hi:[0,1] neg_lo:[0,1]
	v_pk_fma_f32 v[56:57], v[180:181], v[56:57], v[58:59] op_sel_hi:[1,0,1]
	v_pk_mul_f32 v[58:59], v[86:87], v[56:57] op_sel:[1,1] op_sel_hi:[1,0] neg_lo:[1,0]
	v_pk_fma_f32 v[58:59], v[86:87], v[56:57], v[58:59] op_sel_hi:[0,1,1]
	ds_write_b64 v10, v[58:59] offset:29568
	v_pk_mul_f32 v[58:59], v[180:181], v[56:57] op_sel:[1,1] op_sel_hi:[0,1] neg_lo:[0,1]
	v_pk_fma_f32 v[56:57], v[180:181], v[56:57], v[58:59] op_sel_hi:[1,0,1]
	v_pk_mul_f32 v[58:59], v[46:47], v[56:57] op_sel:[1,1] op_sel_hi:[1,0] neg_lo:[1,0]
	v_pk_fma_f32 v[46:47], v[46:47], v[56:57], v[58:59] op_sel_hi:[0,1,1]
	ds_write_b64 v10, v[46:47] offset:33792
	v_pk_mul_f32 v[46:47], v[180:181], v[56:57] op_sel:[1,1] op_sel_hi:[0,1] neg_lo:[0,1]
	v_pk_fma_f32 v[46:47], v[180:181], v[56:57], v[46:47] op_sel_hi:[1,0,1]
	v_pk_mul_f32 v[56:57], v[72:73], v[46:47] op_sel:[1,1] op_sel_hi:[1,0] neg_lo:[1,0]
	v_pk_fma_f32 v[56:57], v[72:73], v[46:47], v[56:57] op_sel_hi:[0,1,1]
	ds_write_b64 v10, v[56:57] offset:38016
	v_pk_mul_f32 v[56:57], v[180:181], v[46:47] op_sel:[1,1] op_sel_hi:[0,1] neg_lo:[0,1]
	v_pk_fma_f32 v[46:47], v[180:181], v[46:47], v[56:57] op_sel_hi:[1,0,1]
	v_pk_mul_f32 v[56:57], v[50:51], v[46:47] op_sel:[1,1] op_sel_hi:[1,0] neg_lo:[1,0]
	v_pk_fma_f32 v[50:51], v[50:51], v[46:47], v[56:57] op_sel_hi:[0,1,1]
	ds_write_b64 v10, v[50:51] offset:42240
	v_pk_mul_f32 v[50:51], v[180:181], v[46:47] op_sel:[1,1] op_sel_hi:[0,1] neg_lo:[0,1]
	v_pk_fma_f32 v[46:47], v[180:181], v[46:47], v[50:51] op_sel_hi:[1,0,1]
	v_pk_mul_f32 v[50:51], v[82:83], v[46:47] op_sel:[1,1] op_sel_hi:[1,0] neg_lo:[1,0]
	v_pk_fma_f32 v[50:51], v[82:83], v[46:47], v[50:51] op_sel_hi:[0,1,1]
	ds_write_b64 v10, v[50:51] offset:46464
	v_pk_mul_f32 v[50:51], v[180:181], v[46:47] op_sel:[1,1] op_sel_hi:[0,1] neg_lo:[0,1]
	v_pk_fma_f32 v[46:47], v[180:181], v[46:47], v[50:51] op_sel_hi:[1,0,1]
	v_pk_mul_f32 v[50:51], v[40:41], v[46:47] op_sel:[1,1] op_sel_hi:[1,0] neg_lo:[1,0]
	v_pk_fma_f32 v[40:41], v[40:41], v[46:47], v[50:51] op_sel_hi:[0,1,1]
	ds_write_b64 v10, v[40:41] offset:50688
	v_pk_mul_f32 v[40:41], v[180:181], v[46:47] op_sel:[1,1] op_sel_hi:[0,1] neg_lo:[0,1]
	v_pk_fma_f32 v[40:41], v[180:181], v[46:47], v[40:41] op_sel_hi:[1,0,1]
	v_pk_mul_f32 v[46:47], v[68:69], v[40:41] op_sel:[1,1] op_sel_hi:[1,0] neg_lo:[1,0]
	v_pk_fma_f32 v[46:47], v[68:69], v[40:41], v[46:47] op_sel_hi:[0,1,1]
	ds_write_b64 v10, v[46:47] offset:54912
	v_pk_mul_f32 v[46:47], v[180:181], v[40:41] op_sel:[1,1] op_sel_hi:[0,1] neg_lo:[0,1]
	v_pk_fma_f32 v[40:41], v[180:181], v[40:41], v[46:47] op_sel_hi:[1,0,1]
	v_pk_mul_f32 v[46:47], v[44:45], v[40:41] op_sel:[1,1] op_sel_hi:[1,0] neg_lo:[1,0]
	v_pk_fma_f32 v[44:45], v[44:45], v[40:41], v[46:47] op_sel_hi:[0,1,1]
	ds_write_b64 v10, v[44:45] offset:59136
	v_pk_mul_f32 v[44:45], v[180:181], v[40:41] op_sel:[1,1] op_sel_hi:[0,1] neg_lo:[0,1]
	v_pk_fma_f32 v[40:41], v[180:181], v[40:41], v[44:45] op_sel_hi:[1,0,1]
	v_pk_mul_f32 v[44:45], v[62:63], v[40:41] op_sel:[1,1] op_sel_hi:[1,0] neg_lo:[1,0]
	v_pk_fma_f32 v[44:45], v[62:63], v[40:41], v[44:45] op_sel_hi:[0,1,1]
	ds_write_b64 v10, v[44:45] offset:63360
	v_pk_mul_f32 v[44:45], v[180:181], v[40:41] op_sel:[1,1] op_sel_hi:[0,1] neg_lo:[0,1]
	v_pk_fma_f32 v[40:41], v[180:181], v[40:41], v[44:45] op_sel_hi:[1,0,1]
	v_pk_mul_f32 v[44:45], v[30:31], v[40:41] op_sel:[1,1] op_sel_hi:[1,0] neg_lo:[1,0]
	v_add_u32_e32 v13, 0x10800, v10
	v_pk_fma_f32 v[30:31], v[30:31], v[40:41], v[44:45] op_sel_hi:[0,1,1]
	ds_write_b64 v13, v[30:31]
	v_pk_mul_f32 v[30:31], v[180:181], v[40:41] op_sel:[1,1] op_sel_hi:[0,1] neg_lo:[0,1]
	v_pk_fma_f32 v[30:31], v[180:181], v[40:41], v[30:31] op_sel_hi:[1,0,1]
	v_pk_mul_f32 v[40:41], v[54:55], v[30:31] op_sel:[1,1] op_sel_hi:[1,0] neg_lo:[1,0]
	v_add_u32_e32 v13, 0x11880, v10
	v_pk_fma_f32 v[40:41], v[54:55], v[30:31], v[40:41] op_sel_hi:[0,1,1]
	ds_write_b64 v13, v[40:41]
	v_pk_mul_f32 v[40:41], v[180:181], v[30:31] op_sel:[1,1] op_sel_hi:[0,1] neg_lo:[0,1]
	v_pk_fma_f32 v[30:31], v[180:181], v[30:31], v[40:41] op_sel_hi:[1,0,1]
	v_pk_mul_f32 v[40:41], v[34:35], v[30:31] op_sel:[1,1] op_sel_hi:[1,0] neg_lo:[1,0]
	v_add_u32_e32 v13, 0x12900, v10
	v_pk_fma_f32 v[34:35], v[34:35], v[30:31], v[40:41] op_sel_hi:[0,1,1]
	ds_write_b64 v13, v[34:35]
	v_pk_mul_f32 v[34:35], v[180:181], v[30:31] op_sel:[1,1] op_sel_hi:[0,1] neg_lo:[0,1]
	v_pk_fma_f32 v[30:31], v[180:181], v[30:31], v[34:35] op_sel_hi:[1,0,1]
	v_pk_mul_f32 v[34:35], v[66:67], v[30:31] op_sel:[1,1] op_sel_hi:[1,0] neg_lo:[1,0]
	v_add_u32_e32 v13, 0x13980, v10
	v_pk_fma_f32 v[34:35], v[66:67], v[30:31], v[34:35] op_sel_hi:[0,1,1]
	ds_write_b64 v13, v[34:35]
	v_pk_mul_f32 v[34:35], v[180:181], v[30:31] op_sel:[1,1] op_sel_hi:[0,1] neg_lo:[0,1]
	v_pk_fma_f32 v[30:31], v[180:181], v[30:31], v[34:35] op_sel_hi:[1,0,1]
	v_pk_mul_f32 v[34:35], v[26:27], v[30:31] op_sel:[1,1] op_sel_hi:[1,0] neg_lo:[1,0]
	v_add_u32_e32 v13, 0x14a00, v10
	v_pk_fma_f32 v[26:27], v[26:27], v[30:31], v[34:35] op_sel_hi:[0,1,1]
	ds_write_b64 v13, v[26:27]
	v_pk_mul_f32 v[26:27], v[180:181], v[30:31] op_sel:[1,1] op_sel_hi:[0,1] neg_lo:[0,1]
	v_pk_fma_f32 v[26:27], v[180:181], v[30:31], v[26:27] op_sel_hi:[1,0,1]
	v_pk_mul_f32 v[30:31], v[48:49], v[26:27] op_sel:[1,1] op_sel_hi:[1,0] neg_lo:[1,0]
	v_add_u32_e32 v13, 0x15a80, v10
	v_pk_fma_f32 v[30:31], v[48:49], v[26:27], v[30:31] op_sel_hi:[0,1,1]
	ds_write_b64 v13, v[30:31]
	v_pk_mul_f32 v[30:31], v[180:181], v[26:27] op_sel:[1,1] op_sel_hi:[0,1] neg_lo:[0,1]
	v_pk_fma_f32 v[26:27], v[180:181], v[26:27], v[30:31] op_sel_hi:[1,0,1]
	v_pk_mul_f32 v[30:31], v[28:29], v[26:27] op_sel:[1,1] op_sel_hi:[1,0] neg_lo:[1,0]
	v_add_u32_e32 v13, 0x16b00, v10
	v_pk_fma_f32 v[28:29], v[28:29], v[26:27], v[30:31] op_sel_hi:[0,1,1]
	ds_write_b64 v13, v[28:29]
	v_pk_mul_f32 v[28:29], v[180:181], v[26:27] op_sel:[1,1] op_sel_hi:[0,1] neg_lo:[0,1]
	v_pk_fma_f32 v[26:27], v[180:181], v[26:27], v[28:29] op_sel_hi:[1,0,1]
	v_pk_mul_f32 v[28:29], v[52:53], v[26:27] op_sel:[1,1] op_sel_hi:[1,0] neg_lo:[1,0]
	v_add_u32_e32 v13, 0x17b80, v10
	v_pk_fma_f32 v[28:29], v[52:53], v[26:27], v[28:29] op_sel_hi:[0,1,1]
	ds_write_b64 v13, v[28:29]
	v_pk_mul_f32 v[28:29], v[180:181], v[26:27] op_sel:[1,1] op_sel_hi:[0,1] neg_lo:[0,1]
	v_pk_fma_f32 v[26:27], v[180:181], v[26:27], v[28:29] op_sel_hi:[1,0,1]
	v_pk_mul_f32 v[28:29], v[22:23], v[26:27] op_sel:[1,1] op_sel_hi:[1,0] neg_lo:[1,0]
	v_add_u32_e32 v13, 0x18c00, v10
	v_pk_fma_f32 v[22:23], v[22:23], v[26:27], v[28:29] op_sel_hi:[0,1,1]
	ds_write_b64 v13, v[22:23]
	v_pk_mul_f32 v[22:23], v[180:181], v[26:27] op_sel:[1,1] op_sel_hi:[0,1] neg_lo:[0,1]
	v_pk_fma_f32 v[22:23], v[180:181], v[26:27], v[22:23] op_sel_hi:[1,0,1]
	v_pk_mul_f32 v[26:27], v[38:39], v[22:23] op_sel:[1,1] op_sel_hi:[1,0] neg_lo:[1,0]
	v_add_u32_e32 v13, 0x19c80, v10
	v_pk_fma_f32 v[26:27], v[38:39], v[22:23], v[26:27] op_sel_hi:[0,1,1]
	ds_write_b64 v13, v[26:27]
	v_pk_mul_f32 v[26:27], v[180:181], v[22:23] op_sel:[1,1] op_sel_hi:[0,1] neg_lo:[0,1]
	v_pk_fma_f32 v[22:23], v[180:181], v[22:23], v[26:27] op_sel_hi:[1,0,1]
	v_pk_mul_f32 v[26:27], v[24:25], v[22:23] op_sel:[1,1] op_sel_hi:[1,0] neg_lo:[1,0]
	v_add_u32_e32 v13, 0x1ad00, v10
	v_pk_fma_f32 v[24:25], v[24:25], v[22:23], v[26:27] op_sel_hi:[0,1,1]
	ds_write_b64 v13, v[24:25]
	v_pk_mul_f32 v[24:25], v[180:181], v[22:23] op_sel:[1,1] op_sel_hi:[0,1] neg_lo:[0,1]
	v_pk_fma_f32 v[22:23], v[180:181], v[22:23], v[24:25] op_sel_hi:[1,0,1]
	v_pk_mul_f32 v[24:25], v[42:43], v[22:23] op_sel:[1,1] op_sel_hi:[1,0] neg_lo:[1,0]
	v_add_u32_e32 v13, 0x1bd80, v10
	v_pk_fma_f32 v[24:25], v[42:43], v[22:23], v[24:25] op_sel_hi:[0,1,1]
	ds_write_b64 v13, v[24:25]
	v_pk_mul_f32 v[24:25], v[180:181], v[22:23] op_sel:[1,1] op_sel_hi:[0,1] neg_lo:[0,1]
	v_pk_fma_f32 v[22:23], v[180:181], v[22:23], v[24:25] op_sel_hi:[1,0,1]
	v_pk_mul_f32 v[24:25], v[18:19], v[22:23] op_sel:[1,1] op_sel_hi:[1,0] neg_lo:[1,0]
	v_add_u32_e32 v13, 0x1ce00, v10
	v_pk_fma_f32 v[18:19], v[18:19], v[22:23], v[24:25] op_sel_hi:[0,1,1]
	ds_write_b64 v13, v[18:19]
	v_pk_mul_f32 v[18:19], v[180:181], v[22:23] op_sel:[1,1] op_sel_hi:[0,1] neg_lo:[0,1]
	v_pk_fma_f32 v[18:19], v[180:181], v[22:23], v[18:19] op_sel_hi:[1,0,1]
	v_pk_mul_f32 v[22:23], v[32:33], v[18:19] op_sel:[1,1] op_sel_hi:[1,0] neg_lo:[1,0]
	v_add_u32_e32 v13, 0x1de80, v10
	v_pk_fma_f32 v[22:23], v[32:33], v[18:19], v[22:23] op_sel_hi:[0,1,1]
	ds_write_b64 v13, v[22:23]
	v_pk_mul_f32 v[22:23], v[180:181], v[18:19] op_sel:[1,1] op_sel_hi:[0,1] neg_lo:[0,1]
	v_pk_fma_f32 v[18:19], v[180:181], v[18:19], v[22:23] op_sel_hi:[1,0,1]
	v_pk_mul_f32 v[22:23], v[20:21], v[18:19] op_sel:[1,1] op_sel_hi:[1,0] neg_lo:[1,0]
	v_add_u32_e32 v13, 0x1ef00, v10
	v_pk_fma_f32 v[20:21], v[20:21], v[18:19], v[22:23] op_sel_hi:[0,1,1]
	ds_write_b64 v13, v[20:21]
	v_pk_mul_f32 v[20:21], v[180:181], v[18:19] op_sel:[1,1] op_sel_hi:[0,1] neg_lo:[0,1]
	v_pk_fma_f32 v[16:17], v[180:181], v[18:19], v[20:21] op_sel_hi:[1,0,1]
	v_pk_mul_f32 v[18:19], v[36:37], v[16:17] op_sel:[1,1] op_sel_hi:[1,0] neg_lo:[1,0]
	v_add_u32_e32 v10, 0x1ff80, v10
	v_pk_fma_f32 v[16:17], v[36:37], v[16:17], v[18:19] op_sel_hi:[0,1,1]
	ds_write_b64 v10, v[16:17]
	v_mov_b32_e32 v10, v176
	v_mov_b32_e32 v13, v173
	s_waitcnt lgkmcnt(0)
	s_barrier
	v_mov_b32_e32 v16, v182
	v_add_u32_e32 v15, v13, v10
	v_lshl_add_u32 v75, v15, 3, 0
	v_xad_u32 v15, v13, 1, v10
	v_lshl_add_u32 v74, v15, 3, 0
	v_xad_u32 v15, v13, 2, v10
	v_lshl_add_u32 v73, v15, 3, 0
	v_xad_u32 v15, v13, 3, v10
	v_lshl_add_u32 v72, v15, 3, 0
	v_xad_u32 v15, v13, 4, v10
	v_lshl_add_u32 v71, v15, 3, 0
	v_xad_u32 v15, v13, 5, v10
	v_lshl_add_u32 v70, v15, 3, 0
	v_xad_u32 v15, v13, 6, v10
	v_lshl_add_u32 v69, v15, 3, 0
	v_xad_u32 v15, v13, 7, v10
	v_lshl_add_u32 v68, v15, 3, 0
	v_xad_u32 v15, v13, 8, v10
	v_lshl_add_u32 v15, v15, 3, 0
	v_add_u32_e32 v67, 0x800, v15
	v_xad_u32 v15, v13, 9, v10
	v_lshl_add_u32 v15, v15, 3, 0
	v_add_u32_e32 v66, 0x800, v15
	v_xad_u32 v15, v13, 10, v10
	v_lshl_add_u32 v15, v15, 3, 0
	v_add_u32_e32 v65, 0x800, v15
	v_xad_u32 v15, v13, 11, v10
	v_lshl_add_u32 v15, v15, 3, 0
	v_add_u32_e32 v64, 0x800, v15
	v_xad_u32 v15, v13, 12, v10
	v_mov_b32_e32 v17, v183
	v_lshl_add_u32 v15, v15, 3, 0
	ds_read2_b64 v[18:21], v75 offset1:16
	ds_read2_b64 v[40:43], v67 offset1:16
	v_add_u32_e32 v63, 0x800, v15
	v_xad_u32 v15, v13, 13, v10
	v_lshl_add_u32 v15, v15, 3, 0
	v_add_u32_e32 v62, 0x800, v15
	v_xad_u32 v15, v13, 14, v10
	v_xad_u32 v10, v13, 15, v10
	ds_read2_b64 v[22:25], v74 offset0:32 offset1:48
	ds_read2_b64 v[48:51], v66 offset0:32 offset1:48
	v_lshl_add_u32 v15, v15, 3, 0
	v_lshl_add_u32 v10, v10, 3, 0
	v_add_u32_e32 v15, 0x800, v15
	v_add_u32_e32 v13, 0x800, v10
	v_mov_b32_e32 v10, v164
	ds_read2_b64 v[26:29], v73 offset0:64 offset1:80
	ds_read2_b64 v[58:61], v72 offset0:96 offset1:112
	ds_read2_b64 v[76:79], v71 offset0:128 offset1:144
	ds_read2_b64 v[80:83], v70 offset0:160 offset1:176
	ds_read2_b64 v[84:87], v69 offset0:192 offset1:208
	ds_read2_b64 v[88:91], v68 offset0:224 offset1:240
	ds_read2_b64 v[54:57], v65 offset0:64 offset1:80
	ds_read2_b64 v[92:95], v64 offset0:96 offset1:112
	ds_read2_b64 v[96:99], v63 offset0:128 offset1:144
	ds_read2_b64 v[100:103], v62 offset0:160 offset1:176
	ds_read2_b64 v[104:107], v15 offset0:192 offset1:208
	ds_read2_b64 v[108:111], v13 offset0:224 offset1:240
	s_waitcnt lgkmcnt(14)
	v_pk_add_f32 v[112:113], v[18:19], v[40:41]
	v_pk_add_f32 v[40:41], v[18:19], v[40:41] neg_lo:[0,1] neg_hi:[0,1]
	v_pk_add_f32 v[18:19], v[20:21], v[42:43]
	v_pk_add_f32 v[20:21], v[20:21], v[42:43] neg_lo:[0,1] neg_hi:[0,1]
	v_mov_b32_e32 v30, v165
	v_mov_b32_e32 v32, v166
	v_mov_b32_e32 v34, v167
	v_mov_b32_e32 v10, v168
	v_mov_b32_e32 v38, v169
	v_mov_b32_e32 v36, v170
	v_mov_b32_e32 v46, v171
	v_mov_b32_e32 v31, v172
	v_pk_mul_f32 v[42:43], v[20:21], v[46:47] op_sel:[1,0] op_sel_hi:[0,0] neg_lo:[1,1] neg_hi:[0,1]
	v_pk_fma_f32 v[44:45], v[20:21], v[30:31], v[42:43] op_sel_hi:[1,0,1]
	s_waitcnt lgkmcnt(12)
	v_pk_add_f32 v[20:21], v[22:23], v[48:49]
	v_pk_add_f32 v[22:23], v[22:23], v[48:49] neg_lo:[0,1] neg_hi:[0,1]
	v_pk_mul_f32 v[42:43], v[22:23], v[36:37] op_sel:[1,0] op_sel_hi:[0,0] neg_lo:[1,1] neg_hi:[0,1]
	v_pk_fma_f32 v[48:49], v[22:23], v[32:33], v[42:43] op_sel_hi:[1,0,1]
	v_pk_add_f32 v[22:23], v[24:25], v[50:51]
	v_pk_add_f32 v[24:25], v[24:25], v[50:51] neg_lo:[0,1] neg_hi:[0,1]
	v_pk_mul_f32 v[42:43], v[24:25], v[38:39] op_sel:[1,0] op_sel_hi:[0,0] neg_lo:[1,1] neg_hi:[0,1]
	v_pk_fma_f32 v[52:53], v[24:25], v[34:35], v[42:43] op_sel_hi:[1,0,1]
	s_waitcnt lgkmcnt(5)
	v_pk_add_f32 v[24:25], v[26:27], v[54:55]
	v_pk_add_f32 v[26:27], v[26:27], v[54:55] neg_lo:[0,1] neg_hi:[0,1]
	v_pk_mul_f32 v[42:43], v[26:27], v[10:11] op_sel:[1,0] op_sel_hi:[0,0] neg_lo:[1,1] neg_hi:[0,1]
	v_pk_fma_f32 v[54:55], v[26:27], v[10:11], v[42:43] op_sel_hi:[1,0,1]
	v_pk_add_f32 v[26:27], v[28:29], v[56:57]
	v_pk_add_f32 v[28:29], v[28:29], v[56:57] neg_lo:[0,1] neg_hi:[0,1]
	v_pk_mul_f32 v[42:43], v[28:29], v[38:39] op_sel_hi:[1,0]
	v_pk_fma_f32 v[56:57], v[28:29], v[34:35], v[42:43] op_sel:[1,0,0] op_sel_hi:[0,0,1] neg_lo:[1,1,0] neg_hi:[0,1,0]
	s_waitcnt lgkmcnt(4)
	v_pk_add_f32 v[42:43], v[58:59], v[92:93] neg_lo:[0,1] neg_hi:[0,1]
	v_pk_add_f32 v[28:29], v[58:59], v[92:93]
	v_pk_mul_f32 v[50:51], v[42:43], v[36:37] op_sel_hi:[1,0]
	v_pk_fma_f32 v[58:59], v[42:43], v[32:33], v[50:51] op_sel:[1,0,0] op_sel_hi:[0,0,1] neg_lo:[1,1,0] neg_hi:[0,1,0]
	v_pk_add_f32 v[50:51], v[60:61], v[94:95] neg_lo:[0,1] neg_hi:[0,1]
	v_pk_add_f32 v[42:43], v[60:61], v[94:95]
	v_pk_mul_f32 v[60:61], v[50:51], v[46:47] op_sel_hi:[1,0]
	v_xor_b32_e32 v92, 0x80000000, v51
	v_mov_b32_e32 v93, v50
	s_waitcnt lgkmcnt(3)
	v_pk_add_f32 v[50:51], v[76:77], v[96:97]
	v_pk_add_f32 v[76:77], v[76:77], v[96:97] neg_lo:[0,1] neg_hi:[0,1]
	v_pk_fma_f32 v[60:61], v[92:93], v[30:31], v[60:61] op_sel_hi:[1,0,1] neg_lo:[0,1,0] neg_hi:[0,1,0]
	v_xor_b32_e32 v93, 0x80000000, v76
	v_mov_b32_e32 v92, v77
	v_pk_add_f32 v[76:77], v[78:79], v[98:99]
	v_pk_add_f32 v[78:79], v[78:79], v[98:99] neg_lo:[0,1] neg_hi:[0,1]
	v_pk_mul_f32 v[94:95], v[78:79], v[46:47] op_sel_hi:[1,0] neg_lo:[0,1] neg_hi:[0,1]
	v_pk_fma_f32 v[78:79], v[78:79], v[30:31], v[94:95] op_sel:[1,0,0] op_sel_hi:[0,0,1] neg_lo:[1,1,0] neg_hi:[0,1,0]
	s_waitcnt lgkmcnt(2)
	v_pk_add_f32 v[94:95], v[80:81], v[100:101]
	v_pk_add_f32 v[80:81], v[80:81], v[100:101] neg_lo:[0,1] neg_hi:[0,1]
	v_pk_mul_f32 v[96:97], v[80:81], v[36:37] op_sel_hi:[1,0] neg_lo:[0,1] neg_hi:[0,1]
	v_pk_fma_f32 v[80:81], v[80:81], v[32:33], v[96:97] op_sel:[1,0,0] op_sel_hi:[0,0,1] neg_lo:[1,1,0] neg_hi:[0,1,0]
	v_pk_add_f32 v[96:97], v[82:83], v[102:103]
	v_pk_add_f32 v[82:83], v[82:83], v[102:103] neg_lo:[0,1] neg_hi:[0,1]
	v_pk_mul_f32 v[98:99], v[82:83], v[38:39] op_sel_hi:[1,0] neg_lo:[0,1] neg_hi:[0,1]
	v_pk_fma_f32 v[82:83], v[82:83], v[34:35], v[98:99] op_sel:[1,0,0] op_sel_hi:[0,0,1] neg_lo:[1,1,0] neg_hi:[0,1,0]
	s_waitcnt lgkmcnt(1)
	v_pk_add_f32 v[98:99], v[84:85], v[104:105]
	v_pk_add_f32 v[84:85], v[84:85], v[104:105] neg_lo:[0,1] neg_hi:[0,1]
	v_pk_mul_f32 v[100:101], v[84:85], v[10:11] op_sel:[1,0] op_sel_hi:[0,0] neg_lo:[1,1] neg_hi:[0,1]
	v_pk_fma_f32 v[84:85], v[84:85], v[10:11], v[100:101] op_sel_hi:[1,0,1] neg_lo:[0,1,0] neg_hi:[0,1,0]
	v_pk_add_f32 v[100:101], v[86:87], v[106:107]
	v_pk_add_f32 v[86:87], v[86:87], v[106:107] neg_lo:[0,1] neg_hi:[0,1]
	v_pk_mul_f32 v[38:39], v[86:87], v[38:39] op_sel:[1,0] op_sel_hi:[0,0] neg_lo:[1,1] neg_hi:[0,1]
	v_pk_fma_f32 v[86:87], v[86:87], v[34:35], v[38:39] op_sel_hi:[1,0,1] neg_lo:[0,1,0] neg_hi:[0,1,0]
	s_waitcnt lgkmcnt(0)
	v_pk_add_f32 v[38:39], v[88:89], v[108:109] neg_lo:[0,1] neg_hi:[0,1]
	v_pk_add_f32 v[34:35], v[88:89], v[108:109]
	v_pk_mul_f32 v[88:89], v[38:39], v[36:37] op_sel:[1,0] op_sel_hi:[0,0] neg_lo:[1,1] neg_hi:[0,1]
	v_pk_fma_f32 v[88:89], v[38:39], v[32:33], v[88:89] op_sel_hi:[1,0,1] neg_lo:[0,1,0] neg_hi:[0,1,0]
	v_pk_add_f32 v[38:39], v[90:91], v[110:111]
	v_pk_add_f32 v[90:91], v[90:91], v[110:111] neg_lo:[0,1] neg_hi:[0,1]
	v_pk_mul_f32 v[46:47], v[90:91], v[46:47] op_sel:[1,0] op_sel_hi:[0,0] neg_lo:[1,1] neg_hi:[0,1]
	v_pk_fma_f32 v[90:91], v[90:91], v[30:31], v[46:47] op_sel_hi:[1,0,1] neg_lo:[0,1,0] neg_hi:[0,1,0]
	v_pk_add_f32 v[46:47], v[18:19], v[76:77]
	v_pk_add_f32 v[18:19], v[18:19], v[76:77] neg_lo:[0,1] neg_hi:[0,1]
	v_pk_add_f32 v[30:31], v[112:113], v[50:51]
	v_pk_mul_f32 v[76:77], v[18:19], v[36:37] op_sel:[1,0] op_sel_hi:[0,0] neg_lo:[1,1] neg_hi:[0,1]
	v_pk_add_f32 v[50:51], v[112:113], v[50:51] neg_lo:[0,1] neg_hi:[0,1]
	v_pk_fma_f32 v[76:77], v[18:19], v[32:33], v[76:77] op_sel_hi:[1,0,1]
	v_pk_add_f32 v[18:19], v[20:21], v[94:95]
	v_pk_add_f32 v[20:21], v[20:21], v[94:95] neg_lo:[0,1] neg_hi:[0,1]
	v_pk_mul_f32 v[94:95], v[20:21], v[10:11] op_sel:[1,0] op_sel_hi:[0,0] neg_lo:[1,1] neg_hi:[0,1]
	v_pk_fma_f32 v[20:21], v[20:21], v[10:11], v[94:95] op_sel_hi:[1,0,1]
	v_pk_add_f32 v[94:95], v[22:23], v[96:97]
	v_pk_add_f32 v[22:23], v[22:23], v[96:97] neg_lo:[0,1] neg_hi:[0,1]
	v_pk_mul_f32 v[96:97], v[22:23], v[36:37] op_sel_hi:[1,0]
	v_xor_b32_e32 v102, 0x80000000, v23
	v_mov_b32_e32 v103, v22
	v_pk_add_f32 v[22:23], v[24:25], v[98:99]
	v_pk_add_f32 v[24:25], v[24:25], v[98:99] neg_lo:[0,1] neg_hi:[0,1]
	v_pk_fma_f32 v[96:97], v[102:103], v[32:33], v[96:97] op_sel_hi:[1,0,1] neg_lo:[0,1,0] neg_hi:[0,1,0]
	v_xor_b32_e32 v99, 0x80000000, v24
	v_mov_b32_e32 v98, v25
	v_pk_add_f32 v[24:25], v[26:27], v[100:101]
	v_pk_add_f32 v[26:27], v[26:27], v[100:101] neg_lo:[0,1] neg_hi:[0,1]
	v_pk_mul_f32 v[100:101], v[26:27], v[36:37] op_sel_hi:[1,0] neg_lo:[0,1] neg_hi:[0,1]
	v_xor_b32_e32 v102, 0x80000000, v27
	v_mov_b32_e32 v103, v26
	v_pk_add_f32 v[26:27], v[28:29], v[34:35]
	v_pk_add_f32 v[28:29], v[28:29], v[34:35] neg_lo:[0,1] neg_hi:[0,1]
	v_pk_fma_f32 v[100:101], v[102:103], v[32:33], v[100:101] op_sel_hi:[1,0,1] neg_lo:[0,1,0] neg_hi:[0,1,0]
	v_pk_mul_f32 v[34:35], v[28:29], v[10:11] op_sel:[1,0] op_sel_hi:[0,0] neg_lo:[1,1] neg_hi:[0,1]
	v_pk_add_f32 v[102:103], v[30:31], v[22:23] neg_lo:[0,1] neg_hi:[0,1]
	v_pk_fma_f32 v[28:29], v[28:29], v[10:11], v[34:35] op_sel_hi:[1,0,1] neg_lo:[0,1,0] neg_hi:[0,1,0]
	v_pk_add_f32 v[34:35], v[42:43], v[38:39]
	v_pk_add_f32 v[38:39], v[42:43], v[38:39] neg_lo:[0,1] neg_hi:[0,1]
	v_pk_mul_f32 v[42:43], v[38:39], v[36:37] op_sel:[1,0] op_sel_hi:[0,0] neg_lo:[1,1] neg_hi:[0,1]
	v_pk_fma_f32 v[42:43], v[38:39], v[32:33], v[42:43] op_sel_hi:[1,0,1] neg_lo:[0,1,0] neg_hi:[0,1,0]
	v_pk_add_f32 v[38:39], v[30:31], v[22:23]
	v_pk_add_f32 v[22:23], v[46:47], v[24:25]
	v_pk_add_f32 v[24:25], v[46:47], v[24:25] neg_lo:[0,1] neg_hi:[0,1]
	v_pk_mul_f32 v[30:31], v[24:25], v[10:11] op_sel:[1,0] op_sel_hi:[0,0] neg_lo:[1,1] neg_hi:[0,1]
	v_pk_fma_f32 v[24:25], v[24:25], v[10:11], v[30:31] op_sel_hi:[1,0,1]
	v_pk_add_f32 v[30:31], v[18:19], v[26:27]
	v_pk_add_f32 v[18:19], v[18:19], v[26:27] neg_lo:[0,1] neg_hi:[0,1]
	v_xor_b32_e32 v27, 0x80000000, v18
	v_mov_b32_e32 v26, v19
	v_pk_add_f32 v[18:19], v[94:95], v[34:35]
	v_pk_add_f32 v[34:35], v[94:95], v[34:35] neg_lo:[0,1] neg_hi:[0,1]
	v_pk_mul_f32 v[46:47], v[34:35], v[10:11] op_sel:[1,0] op_sel_hi:[0,0] neg_lo:[1,1] neg_hi:[0,1]
	v_pk_fma_f32 v[34:35], v[34:35], v[10:11], v[46:47] op_sel_hi:[1,0,1] neg_lo:[0,1,0] neg_hi:[0,1,0]
	v_pk_add_f32 v[46:47], v[38:39], v[30:31]
	v_pk_add_f32 v[38:39], v[38:39], v[30:31] neg_lo:[0,1] neg_hi:[0,1]
	v_pk_add_f32 v[30:31], v[22:23], v[18:19]
	v_pk_add_f32 v[18:19], v[22:23], v[18:19] neg_lo:[0,1] neg_hi:[0,1]
	v_pk_add_f32 v[94:95], v[46:47], v[30:31]
	v_xor_b32_e32 v23, 0x80000000, v18
	v_mov_b32_e32 v22, v19
	v_pk_add_f32 v[18:19], v[102:103], v[26:27]
	v_pk_add_f32 v[102:103], v[102:103], v[26:27] neg_lo:[0,1] neg_hi:[0,1]
	v_pk_add_f32 v[26:27], v[24:25], v[34:35]
	v_pk_add_f32 v[24:25], v[24:25], v[34:35] neg_lo:[0,1] neg_hi:[0,1]
	v_pk_add_f32 v[30:31], v[46:47], v[30:31] neg_lo:[0,1] neg_hi:[0,1]
	v_xor_b32_e32 v35, 0x80000000, v24
	v_mov_b32_e32 v34, v25
	v_pk_add_f32 v[24:25], v[50:51], v[98:99]
	v_pk_add_f32 v[98:99], v[50:51], v[98:99] neg_lo:[0,1] neg_hi:[0,1]
	v_pk_add_f32 v[50:51], v[76:77], v[100:101] neg_lo:[0,1] neg_hi:[0,1]
	v_pk_add_f32 v[46:47], v[38:39], v[22:23]
	v_pk_add_f32 v[22:23], v[38:39], v[22:23] neg_lo:[0,1] neg_hi:[0,1]
	v_pk_add_f32 v[104:105], v[18:19], v[26:27]
	v_pk_add_f32 v[26:27], v[18:19], v[26:27] neg_lo:[0,1] neg_hi:[0,1]
	v_pk_add_f32 v[38:39], v[102:103], v[34:35]
	v_pk_add_f32 v[18:19], v[102:103], v[34:35] neg_lo:[0,1] neg_hi:[0,1]
	v_pk_add_f32 v[34:35], v[76:77], v[100:101]
	v_pk_mul_f32 v[76:77], v[10:11], v[50:51] op_sel:[0,1] op_sel_hi:[0,0] neg_lo:[1,1] neg_hi:[1,0]
	v_pk_fma_f32 v[76:77], v[10:11], v[50:51], v[76:77] op_sel_hi:[0,1,1]
	v_pk_add_f32 v[50:51], v[20:21], v[28:29]
	v_pk_add_f32 v[20:21], v[20:21], v[28:29] neg_lo:[0,1] neg_hi:[0,1]
	v_xor_b32_e32 v29, 0x80000000, v20
	v_mov_b32_e32 v28, v21
	v_pk_add_f32 v[20:21], v[96:97], v[42:43]
	v_pk_add_f32 v[42:43], v[96:97], v[42:43] neg_lo:[0,1] neg_hi:[0,1]
	v_pk_mul_f32 v[96:97], v[10:11], v[42:43] op_sel:[0,1] op_sel_hi:[0,0] neg_lo:[1,1] neg_hi:[1,0]
	v_pk_fma_f32 v[42:43], v[10:11], v[42:43], v[96:97] op_sel_hi:[0,1,1] neg_lo:[1,0,0] neg_hi:[1,0,0]
	v_pk_add_f32 v[96:97], v[24:25], v[50:51]
	v_pk_add_f32 v[24:25], v[24:25], v[50:51] neg_lo:[0,1] neg_hi:[0,1]
	v_pk_add_f32 v[50:51], v[34:35], v[20:21]
	v_pk_add_f32 v[20:21], v[34:35], v[20:21] neg_lo:[0,1] neg_hi:[0,1]
	v_pk_add_f32 v[102:103], v[96:97], v[50:51]
	v_xor_b32_e32 v101, 0x80000000, v20
	v_mov_b32_e32 v100, v21
	v_pk_add_f32 v[34:35], v[96:97], v[50:51] neg_lo:[0,1] neg_hi:[0,1]
	v_pk_add_f32 v[20:21], v[98:99], v[28:29]
	v_pk_add_f32 v[96:97], v[98:99], v[28:29] neg_lo:[0,1] neg_hi:[0,1]
	v_pk_add_f32 v[28:29], v[76:77], v[42:43]
	v_pk_add_f32 v[42:43], v[76:77], v[42:43] neg_lo:[0,1] neg_hi:[0,1]
	v_pk_add_f32 v[98:99], v[20:21], v[28:29]
	v_xor_b32_e32 v77, 0x80000000, v42
	v_mov_b32_e32 v76, v43
	v_pk_add_f32 v[28:29], v[20:21], v[28:29] neg_lo:[0,1] neg_hi:[0,1]
	v_pk_add_f32 v[42:43], v[96:97], v[76:77]
	v_pk_add_f32 v[20:21], v[96:97], v[76:77] neg_lo:[0,1] neg_hi:[0,1]
	v_pk_add_f32 v[76:77], v[40:41], v[92:93]
	v_pk_add_f32 v[92:93], v[40:41], v[92:93] neg_lo:[0,1] neg_hi:[0,1]
	v_pk_add_f32 v[40:41], v[44:45], v[78:79]
	v_pk_add_f32 v[44:45], v[44:45], v[78:79] neg_lo:[0,1] neg_hi:[0,1]
	v_pk_add_f32 v[50:51], v[24:25], v[100:101]
	v_pk_mul_f32 v[78:79], v[36:37], v[44:45] op_sel:[0,1] op_sel_hi:[0,0] neg_lo:[1,1] neg_hi:[1,0]
	v_pk_fma_f32 v[44:45], v[32:33], v[44:45], v[78:79] op_sel_hi:[0,1,1]
	v_pk_add_f32 v[78:79], v[48:49], v[80:81]
	v_pk_add_f32 v[48:49], v[48:49], v[80:81] neg_lo:[0,1] neg_hi:[0,1]
	v_pk_add_f32 v[24:25], v[24:25], v[100:101] neg_lo:[0,1] neg_hi:[0,1]
	v_pk_mul_f32 v[80:81], v[10:11], v[48:49] op_sel:[0,1] op_sel_hi:[0,0] neg_lo:[1,1] neg_hi:[1,0]
	v_pk_fma_f32 v[80:81], v[10:11], v[48:49], v[80:81] op_sel_hi:[0,1,1]
	v_pk_add_f32 v[48:49], v[52:53], v[82:83]
	v_pk_add_f32 v[52:53], v[52:53], v[82:83] neg_lo:[0,1] neg_hi:[0,1]
	v_pk_mul_f32 v[82:83], v[32:33], v[52:53] op_sel:[0,1] op_sel_hi:[0,0] neg_lo:[1,1] neg_hi:[1,0]
	v_pk_fma_f32 v[52:53], v[36:37], v[52:53], v[82:83] op_sel_hi:[0,1,1]
	v_pk_add_f32 v[82:83], v[54:55], v[84:85]
	v_pk_add_f32 v[54:55], v[54:55], v[84:85] neg_lo:[0,1] neg_hi:[0,1]
	v_xor_b32_e32 v85, 0x80000000, v54
	v_mov_b32_e32 v84, v55
	v_pk_add_f32 v[54:55], v[56:57], v[86:87]
	v_pk_add_f32 v[56:57], v[56:57], v[86:87] neg_lo:[0,1] neg_hi:[0,1]
	v_pk_mul_f32 v[86:87], v[32:33], v[56:57] op_sel:[0,1] op_sel_hi:[0,0] neg_lo:[1,1] neg_hi:[1,0]
	v_pk_fma_f32 v[56:57], v[36:37], v[56:57], v[86:87] op_sel_hi:[0,1,1] neg_lo:[1,0,0] neg_hi:[1,0,0]
	v_pk_add_f32 v[86:87], v[58:59], v[88:89]
	v_pk_add_f32 v[58:59], v[58:59], v[88:89] neg_lo:[0,1] neg_hi:[0,1]
	v_pk_mul_f32 v[88:89], v[10:11], v[58:59] op_sel:[0,1] op_sel_hi:[0,0] neg_lo:[1,1] neg_hi:[1,0]
	v_pk_fma_f32 v[58:59], v[10:11], v[58:59], v[88:89] op_sel_hi:[0,1,1] neg_lo:[1,0,0] neg_hi:[1,0,0]
	v_pk_add_f32 v[88:89], v[60:61], v[90:91]
	v_pk_add_f32 v[60:61], v[60:61], v[90:91] neg_lo:[0,1] neg_hi:[0,1]
	v_pk_mul_f32 v[36:37], v[36:37], v[60:61] op_sel:[0,1] op_sel_hi:[0,0] neg_lo:[1,1] neg_hi:[1,0]
	v_pk_fma_f32 v[36:37], v[32:33], v[60:61], v[36:37] op_sel_hi:[0,1,1] neg_lo:[1,0,0] neg_hi:[1,0,0]
	v_pk_add_f32 v[32:33], v[76:77], v[82:83]
	v_pk_add_f32 v[60:61], v[76:77], v[82:83] neg_lo:[0,1] neg_hi:[0,1]
	v_pk_add_f32 v[76:77], v[54:55], v[40:41]
	v_pk_add_f32 v[40:41], v[40:41], v[54:55] neg_lo:[0,1] neg_hi:[0,1]
	v_pk_mul_f32 v[54:55], v[10:11], v[40:41] op_sel:[0,1] op_sel_hi:[0,0] neg_lo:[1,1] neg_hi:[1,0]
	v_pk_fma_f32 v[54:55], v[10:11], v[40:41], v[54:55] op_sel_hi:[0,1,1]
	v_pk_add_f32 v[40:41], v[78:79], v[86:87]
	v_pk_add_f32 v[78:79], v[78:79], v[86:87] neg_lo:[0,1] neg_hi:[0,1]
	v_xor_b32_e32 v83, 0x80000000, v78
	v_mov_b32_e32 v82, v79
	v_pk_add_f32 v[78:79], v[48:49], v[88:89]
	v_pk_add_f32 v[48:49], v[48:49], v[88:89] neg_lo:[0,1] neg_hi:[0,1]
	v_pk_add_f32 v[88:89], v[76:77], v[78:79]
	v_pk_mul_f32 v[86:87], v[10:11], v[48:49] op_sel:[0,1] op_sel_hi:[0,0] neg_lo:[1,1] neg_hi:[1,0]
	v_pk_fma_f32 v[48:49], v[10:11], v[48:49], v[86:87] op_sel_hi:[0,1,1] neg_lo:[1,0,0] neg_hi:[1,0,0]
	v_pk_add_f32 v[86:87], v[32:33], v[40:41]
	v_pk_add_f32 v[32:33], v[32:33], v[40:41] neg_lo:[0,1] neg_hi:[0,1]
	v_pk_add_f32 v[40:41], v[76:77], v[78:79] neg_lo:[0,1] neg_hi:[0,1]
	v_pk_add_f32 v[78:79], v[86:87], v[88:89] neg_lo:[0,1] neg_hi:[0,1]
	v_pk_add_f32 v[90:91], v[32:33], v[40:41] op_sel:[0,1] op_sel_hi:[1,0] neg_hi:[0,1]
	v_pk_add_f32 v[40:41], v[32:33], v[40:41] op_sel:[0,1] op_sel_hi:[1,0] neg_lo:[0,1]
	v_pk_add_f32 v[76:77], v[54:55], v[48:49]
	v_pk_add_f32 v[48:49], v[54:55], v[48:49] neg_lo:[0,1] neg_hi:[0,1]
	v_pk_add_f32 v[32:33], v[60:61], v[82:83]
	v_pk_add_f32 v[60:61], v[60:61], v[82:83] neg_lo:[0,1] neg_hi:[0,1]
	v_xor_b32_e32 v55, 0x80000000, v48
	v_mov_b32_e32 v54, v49
	v_pk_add_f32 v[82:83], v[32:33], v[76:77]
	v_pk_add_f32 v[48:49], v[32:33], v[76:77] neg_lo:[0,1] neg_hi:[0,1]
	v_pk_add_f32 v[76:77], v[60:61], v[54:55]
	v_pk_add_f32 v[32:33], v[60:61], v[54:55] neg_lo:[0,1] neg_hi:[0,1]
	v_pk_add_f32 v[54:55], v[92:93], v[84:85]
	v_pk_add_f32 v[60:61], v[92:93], v[84:85] neg_lo:[0,1] neg_hi:[0,1]
	v_pk_add_f32 v[84:85], v[56:57], v[44:45]
	v_pk_add_f32 v[44:45], v[44:45], v[56:57] neg_lo:[0,1] neg_hi:[0,1]
	v_pk_add_f32 v[86:87], v[86:87], v[88:89]
	v_pk_mul_f32 v[56:57], v[10:11], v[44:45] op_sel:[0,1] op_sel_hi:[0,0] neg_lo:[1,1] neg_hi:[1,0]
	v_pk_fma_f32 v[56:57], v[10:11], v[44:45], v[56:57] op_sel_hi:[0,1,1]
	v_pk_add_f32 v[44:45], v[80:81], v[58:59]
	v_pk_add_f32 v[58:59], v[80:81], v[58:59] neg_lo:[0,1] neg_hi:[0,1]
	v_xor_b32_e32 v81, 0x80000000, v58
	v_mov_b32_e32 v80, v59
	v_pk_add_f32 v[58:59], v[52:53], v[36:37]
	v_pk_add_f32 v[36:37], v[52:53], v[36:37] neg_lo:[0,1] neg_hi:[0,1]
	v_pk_mul_f32 v[52:53], v[10:11], v[36:37] op_sel:[0,1] op_sel_hi:[0,0] neg_lo:[1,1] neg_hi:[1,0]
	v_pk_fma_f32 v[36:37], v[10:11], v[36:37], v[52:53] op_sel_hi:[0,1,1] neg_lo:[1,0,0] neg_hi:[1,0,0]
	v_pk_add_f32 v[52:53], v[54:55], v[44:45]
	v_pk_add_f32 v[44:45], v[54:55], v[44:45] neg_lo:[0,1] neg_hi:[0,1]
	v_pk_add_f32 v[54:55], v[84:85], v[58:59]
	v_pk_add_f32 v[58:59], v[84:85], v[58:59] neg_lo:[0,1] neg_hi:[0,1]
	v_xor_b32_e32 v85, 0x80000000, v58
	v_mov_b32_e32 v84, v59
	v_pk_add_f32 v[58:59], v[52:53], v[54:55]
	v_pk_add_f32 v[52:53], v[52:53], v[54:55] neg_lo:[0,1] neg_hi:[0,1]
	v_pk_add_f32 v[54:55], v[44:45], v[84:85]
	v_pk_add_f32 v[44:45], v[44:45], v[84:85] neg_lo:[0,1] neg_hi:[0,1]
	v_pk_add_f32 v[84:85], v[60:61], v[80:81]
	v_pk_add_f32 v[60:61], v[60:61], v[80:81] neg_lo:[0,1] neg_hi:[0,1]
	v_pk_add_f32 v[80:81], v[56:57], v[36:37]
	v_pk_add_f32 v[36:37], v[56:57], v[36:37] neg_lo:[0,1] neg_hi:[0,1]
	v_pk_add_f32 v[92:93], v[84:85], v[80:81]
	v_pk_add_f32 v[80:81], v[84:85], v[80:81] neg_lo:[0,1] neg_hi:[0,1]
	v_pk_add_f32 v[84:85], v[60:61], v[36:37] op_sel:[0,1] op_sel_hi:[1,0] neg_hi:[0,1]
	v_pk_add_f32 v[36:37], v[60:61], v[36:37] op_sel:[0,1] op_sel_hi:[1,0] neg_lo:[0,1]
	v_pk_fma_f32 v[60:61], v[16:17], s[92:93], v[16:17] op_sel:[1,0,0] op_sel_hi:[0,1,1]
	v_pk_mul_f32 v[56:57], v[94:95], s[14:15] op_sel:[1,0] neg_lo:[1,0]
	v_pk_mul_f32 v[88:89], v[60:61], v[86:87] op_sel:[1,1] op_sel_hi:[0,1] neg_lo:[0,1]
	v_pk_fma_f32 v[56:57], v[94:95], s[42:43], v[56:57] op_sel_hi:[0,1,1]
	v_pk_fma_f32 v[86:87], v[60:61], v[86:87], v[88:89] op_sel_hi:[1,0,1]
	ds_write2_b64 v75, v[56:57], v[86:87] offset1:16
	v_pk_mul_f32 v[56:57], v[16:17], v[60:61] op_sel:[1,1] op_sel_hi:[0,1] neg_lo:[0,1]
	v_pk_fma_f32 v[56:57], v[16:17], v[60:61], v[56:57] op_sel_hi:[1,0,1]
	v_pk_mul_f32 v[60:61], v[56:57], v[102:103] op_sel:[1,1] op_sel_hi:[0,1] neg_lo:[0,1]
	v_pk_mul_f32 v[86:87], v[16:17], v[56:57] op_sel:[1,1] op_sel_hi:[0,1] neg_lo:[0,1]
	v_pk_fma_f32 v[60:61], v[56:57], v[102:103], v[60:61] op_sel_hi:[1,0,1]
	v_pk_fma_f32 v[56:57], v[16:17], v[56:57], v[86:87] op_sel_hi:[1,0,1]
	v_pk_mul_f32 v[86:87], v[56:57], v[58:59] op_sel:[1,1] op_sel_hi:[0,1] neg_lo:[0,1]
	v_pk_fma_f32 v[58:59], v[56:57], v[58:59], v[86:87] op_sel_hi:[1,0,1]
	ds_write2_b64 v74, v[60:61], v[58:59] offset0:32 offset1:48
	v_pk_mul_f32 v[58:59], v[16:17], v[56:57] op_sel:[1,1] op_sel_hi:[0,1] neg_lo:[0,1]
	v_pk_fma_f32 v[56:57], v[16:17], v[56:57], v[58:59] op_sel_hi:[1,0,1]
	v_pk_mul_f32 v[58:59], v[56:57], v[104:105] op_sel:[1,1] op_sel_hi:[0,1] neg_lo:[0,1]
	v_pk_mul_f32 v[60:61], v[16:17], v[56:57] op_sel:[1,1] op_sel_hi:[0,1] neg_lo:[0,1]
	v_pk_fma_f32 v[58:59], v[56:57], v[104:105], v[58:59] op_sel_hi:[1,0,1]
	v_pk_fma_f32 v[56:57], v[16:17], v[56:57], v[60:61] op_sel_hi:[1,0,1]
	v_pk_mul_f32 v[60:61], v[56:57], v[82:83] op_sel:[1,1] op_sel_hi:[0,1] neg_lo:[0,1]
	v_pk_fma_f32 v[60:61], v[56:57], v[82:83], v[60:61] op_sel_hi:[1,0,1]
	ds_write2_b64 v73, v[58:59], v[60:61] offset0:64 offset1:80
	v_pk_mul_f32 v[58:59], v[16:17], v[56:57] op_sel:[1,1] op_sel_hi:[0,1] neg_lo:[0,1]
	v_pk_fma_f32 v[56:57], v[16:17], v[56:57], v[58:59] op_sel_hi:[1,0,1]
	v_pk_mul_f32 v[58:59], v[56:57], v[98:99] op_sel:[1,1] op_sel_hi:[0,1] neg_lo:[0,1]
	v_pk_mul_f32 v[60:61], v[16:17], v[56:57] op_sel:[1,1] op_sel_hi:[0,1] neg_lo:[0,1]
	v_pk_fma_f32 v[58:59], v[56:57], v[98:99], v[58:59] op_sel_hi:[1,0,1]
	v_pk_fma_f32 v[56:57], v[16:17], v[56:57], v[60:61] op_sel_hi:[1,0,1]
	v_pk_mul_f32 v[60:61], v[56:57], v[92:93] op_sel:[1,1] op_sel_hi:[0,1] neg_lo:[0,1]
	v_pk_fma_f32 v[60:61], v[56:57], v[92:93], v[60:61] op_sel_hi:[1,0,1]
	ds_write2_b64 v72, v[58:59], v[60:61] offset0:96 offset1:112
	v_pk_mul_f32 v[58:59], v[16:17], v[56:57] op_sel:[1,1] op_sel_hi:[0,1] neg_lo:[0,1]
	v_pk_fma_f32 v[56:57], v[16:17], v[56:57], v[58:59] op_sel_hi:[1,0,1]
	v_pk_mul_f32 v[58:59], v[56:57], v[46:47] op_sel:[1,1] op_sel_hi:[0,1] neg_lo:[0,1]
	v_pk_fma_f32 v[46:47], v[56:57], v[46:47], v[58:59] op_sel_hi:[1,0,1]
	v_pk_mul_f32 v[58:59], v[16:17], v[56:57] op_sel:[1,1] op_sel_hi:[0,1] neg_lo:[0,1]
	v_pk_fma_f32 v[56:57], v[16:17], v[56:57], v[58:59] op_sel_hi:[1,0,1]
	v_pk_mul_f32 v[58:59], v[56:57], v[90:91] op_sel:[1,1] op_sel_hi:[0,1] neg_lo:[0,1]
	v_pk_fma_f32 v[58:59], v[56:57], v[90:91], v[58:59] op_sel_hi:[1,0,1]
	ds_write2_b64 v71, v[46:47], v[58:59] offset0:128 offset1:144
	v_pk_mul_f32 v[46:47], v[16:17], v[56:57] op_sel:[1,1] op_sel_hi:[0,1] neg_lo:[0,1]
	v_pk_fma_f32 v[46:47], v[16:17], v[56:57], v[46:47] op_sel_hi:[1,0,1]
	v_pk_mul_f32 v[56:57], v[46:47], v[50:51] op_sel:[1,1] op_sel_hi:[0,1] neg_lo:[0,1]
	v_pk_fma_f32 v[50:51], v[46:47], v[50:51], v[56:57] op_sel_hi:[1,0,1]
	v_pk_mul_f32 v[56:57], v[16:17], v[46:47] op_sel:[1,1] op_sel_hi:[0,1] neg_lo:[0,1]
	v_pk_fma_f32 v[46:47], v[16:17], v[46:47], v[56:57] op_sel_hi:[1,0,1]
	v_pk_mul_f32 v[56:57], v[46:47], v[54:55] op_sel:[1,1] op_sel_hi:[0,1] neg_lo:[0,1]
	v_pk_fma_f32 v[54:55], v[46:47], v[54:55], v[56:57] op_sel_hi:[1,0,1]
	ds_write2_b64 v70, v[50:51], v[54:55] offset0:160 offset1:176
	v_pk_mul_f32 v[50:51], v[16:17], v[46:47] op_sel:[1,1] op_sel_hi:[0,1] neg_lo:[0,1]
	v_pk_fma_f32 v[46:47], v[16:17], v[46:47], v[50:51] op_sel_hi:[1,0,1]
	v_pk_mul_f32 v[50:51], v[38:39], v[46:47] op_sel:[1,1] op_sel_hi:[1,0] neg_lo:[1,0]
	v_pk_fma_f32 v[38:39], v[38:39], v[46:47], v[50:51] op_sel_hi:[0,1,1]
	v_pk_mul_f32 v[50:51], v[16:17], v[46:47] op_sel:[1,1] op_sel_hi:[0,1] neg_lo:[0,1]
	v_pk_fma_f32 v[46:47], v[16:17], v[46:47], v[50:51] op_sel_hi:[1,0,1]
	v_pk_mul_f32 v[50:51], v[46:47], v[76:77] op_sel:[1,1] op_sel_hi:[0,1] neg_lo:[0,1]
	v_pk_fma_f32 v[50:51], v[46:47], v[76:77], v[50:51] op_sel_hi:[1,0,1]
	ds_write2_b64 v69, v[38:39], v[50:51] offset0:192 offset1:208
	v_pk_mul_f32 v[38:39], v[16:17], v[46:47] op_sel:[1,1] op_sel_hi:[0,1] neg_lo:[0,1]
	v_pk_fma_f32 v[38:39], v[16:17], v[46:47], v[38:39] op_sel_hi:[1,0,1]
	v_pk_mul_f32 v[46:47], v[42:43], v[38:39] op_sel:[1,1] op_sel_hi:[1,0] neg_lo:[1,0]
	v_pk_fma_f32 v[42:43], v[42:43], v[38:39], v[46:47] op_sel_hi:[0,1,1]
	v_pk_mul_f32 v[46:47], v[16:17], v[38:39] op_sel:[1,1] op_sel_hi:[0,1] neg_lo:[0,1]
	v_pk_fma_f32 v[38:39], v[16:17], v[38:39], v[46:47] op_sel_hi:[1,0,1]
	v_pk_mul_f32 v[46:47], v[38:39], v[84:85] op_sel:[1,1] op_sel_hi:[0,1] neg_lo:[0,1]
	v_pk_fma_f32 v[46:47], v[38:39], v[84:85], v[46:47] op_sel_hi:[1,0,1]
	ds_write2_b64 v68, v[42:43], v[46:47] offset0:224 offset1:240
	v_pk_mul_f32 v[42:43], v[16:17], v[38:39] op_sel:[1,1] op_sel_hi:[0,1] neg_lo:[0,1]
	v_pk_fma_f32 v[38:39], v[16:17], v[38:39], v[42:43] op_sel_hi:[1,0,1]
	v_pk_mul_f32 v[42:43], v[30:31], v[38:39] op_sel:[1,1] op_sel_hi:[1,0] neg_lo:[1,0]
	v_pk_fma_f32 v[30:31], v[30:31], v[38:39], v[42:43] op_sel_hi:[0,1,1]
	v_pk_mul_f32 v[42:43], v[16:17], v[38:39] op_sel:[1,1] op_sel_hi:[0,1] neg_lo:[0,1]
	v_pk_fma_f32 v[38:39], v[16:17], v[38:39], v[42:43] op_sel_hi:[1,0,1]
	v_pk_mul_f32 v[42:43], v[78:79], v[38:39] op_sel:[1,1] op_sel_hi:[1,0] neg_lo:[1,0]
	v_pk_fma_f32 v[42:43], v[78:79], v[38:39], v[42:43] op_sel_hi:[0,1,1]
	ds_write2_b64 v67, v[30:31], v[42:43] offset1:16
	v_pk_mul_f32 v[30:31], v[16:17], v[38:39] op_sel:[1,1] op_sel_hi:[0,1] neg_lo:[0,1]
	v_pk_fma_f32 v[30:31], v[16:17], v[38:39], v[30:31] op_sel_hi:[1,0,1]
	v_pk_mul_f32 v[38:39], v[34:35], v[30:31] op_sel:[1,1] op_sel_hi:[1,0] neg_lo:[1,0]
	v_pk_fma_f32 v[34:35], v[34:35], v[30:31], v[38:39] op_sel_hi:[0,1,1]
	v_pk_mul_f32 v[38:39], v[16:17], v[30:31] op_sel:[1,1] op_sel_hi:[0,1] neg_lo:[0,1]
	v_pk_fma_f32 v[30:31], v[16:17], v[30:31], v[38:39] op_sel_hi:[1,0,1]
	v_pk_mul_f32 v[38:39], v[52:53], v[30:31] op_sel:[1,1] op_sel_hi:[1,0] neg_lo:[1,0]
	v_pk_fma_f32 v[38:39], v[52:53], v[30:31], v[38:39] op_sel_hi:[0,1,1]
	ds_write2_b64 v66, v[34:35], v[38:39] offset0:32 offset1:48
	v_pk_mul_f32 v[34:35], v[16:17], v[30:31] op_sel:[1,1] op_sel_hi:[0,1] neg_lo:[0,1]
	v_pk_fma_f32 v[30:31], v[16:17], v[30:31], v[34:35] op_sel_hi:[1,0,1]
	v_pk_mul_f32 v[34:35], v[26:27], v[30:31] op_sel:[1,1] op_sel_hi:[1,0] neg_lo:[1,0]
	v_pk_fma_f32 v[26:27], v[26:27], v[30:31], v[34:35] op_sel_hi:[0,1,1]
	v_pk_mul_f32 v[34:35], v[16:17], v[30:31] op_sel:[1,1] op_sel_hi:[0,1] neg_lo:[0,1]
	v_pk_fma_f32 v[30:31], v[16:17], v[30:31], v[34:35] op_sel_hi:[1,0,1]
	v_pk_mul_f32 v[34:35], v[48:49], v[30:31] op_sel:[1,1] op_sel_hi:[1,0] neg_lo:[1,0]
	v_pk_fma_f32 v[34:35], v[48:49], v[30:31], v[34:35] op_sel_hi:[0,1,1]
	ds_write2_b64 v65, v[26:27], v[34:35] offset0:64 offset1:80
	v_pk_mul_f32 v[26:27], v[16:17], v[30:31] op_sel:[1,1] op_sel_hi:[0,1] neg_lo:[0,1]
	v_pk_fma_f32 v[26:27], v[16:17], v[30:31], v[26:27] op_sel_hi:[1,0,1]
	v_pk_mul_f32 v[30:31], v[28:29], v[26:27] op_sel:[1,1] op_sel_hi:[1,0] neg_lo:[1,0]
	v_pk_fma_f32 v[28:29], v[28:29], v[26:27], v[30:31] op_sel_hi:[0,1,1]
	v_pk_mul_f32 v[30:31], v[16:17], v[26:27] op_sel:[1,1] op_sel_hi:[0,1] neg_lo:[0,1]
	v_pk_fma_f32 v[26:27], v[16:17], v[26:27], v[30:31] op_sel_hi:[1,0,1]
	v_pk_mul_f32 v[30:31], v[80:81], v[26:27] op_sel:[1,1] op_sel_hi:[1,0] neg_lo:[1,0]
	v_pk_fma_f32 v[30:31], v[80:81], v[26:27], v[30:31] op_sel_hi:[0,1,1]
	ds_write2_b64 v64, v[28:29], v[30:31] offset0:96 offset1:112
	v_pk_mul_f32 v[28:29], v[16:17], v[26:27] op_sel:[1,1] op_sel_hi:[0,1] neg_lo:[0,1]
	v_pk_fma_f32 v[26:27], v[16:17], v[26:27], v[28:29] op_sel_hi:[1,0,1]
	v_pk_mul_f32 v[28:29], v[22:23], v[26:27] op_sel:[1,1] op_sel_hi:[1,0] neg_lo:[1,0]
	v_pk_fma_f32 v[22:23], v[22:23], v[26:27], v[28:29] op_sel_hi:[0,1,1]
	v_pk_mul_f32 v[28:29], v[16:17], v[26:27] op_sel:[1,1] op_sel_hi:[0,1] neg_lo:[0,1]
	v_pk_fma_f32 v[26:27], v[16:17], v[26:27], v[28:29] op_sel_hi:[1,0,1]
	v_pk_mul_f32 v[28:29], v[40:41], v[26:27] op_sel:[1,1] op_sel_hi:[1,0] neg_lo:[1,0]
	v_pk_fma_f32 v[28:29], v[40:41], v[26:27], v[28:29] op_sel_hi:[0,1,1]
	ds_write2_b64 v63, v[22:23], v[28:29] offset0:128 offset1:144
	v_pk_mul_f32 v[22:23], v[16:17], v[26:27] op_sel:[1,1] op_sel_hi:[0,1] neg_lo:[0,1]
	v_pk_fma_f32 v[22:23], v[16:17], v[26:27], v[22:23] op_sel_hi:[1,0,1]
	v_pk_mul_f32 v[26:27], v[24:25], v[22:23] op_sel:[1,1] op_sel_hi:[1,0] neg_lo:[1,0]
	v_pk_fma_f32 v[24:25], v[24:25], v[22:23], v[26:27] op_sel_hi:[0,1,1]
	v_pk_mul_f32 v[26:27], v[16:17], v[22:23] op_sel:[1,1] op_sel_hi:[0,1] neg_lo:[0,1]
	v_pk_fma_f32 v[22:23], v[16:17], v[22:23], v[26:27] op_sel_hi:[1,0,1]
	v_pk_mul_f32 v[26:27], v[44:45], v[22:23] op_sel:[1,1] op_sel_hi:[1,0] neg_lo:[1,0]
	v_pk_fma_f32 v[26:27], v[44:45], v[22:23], v[26:27] op_sel_hi:[0,1,1]
	ds_write2_b64 v62, v[24:25], v[26:27] offset0:160 offset1:176
	v_pk_mul_f32 v[24:25], v[16:17], v[22:23] op_sel:[1,1] op_sel_hi:[0,1] neg_lo:[0,1]
	v_pk_fma_f32 v[22:23], v[16:17], v[22:23], v[24:25] op_sel_hi:[1,0,1]
	v_pk_mul_f32 v[24:25], v[18:19], v[22:23] op_sel:[1,1] op_sel_hi:[1,0] neg_lo:[1,0]
	v_pk_fma_f32 v[18:19], v[18:19], v[22:23], v[24:25] op_sel_hi:[0,1,1]
	v_pk_mul_f32 v[24:25], v[16:17], v[22:23] op_sel:[1,1] op_sel_hi:[0,1] neg_lo:[0,1]
	v_pk_fma_f32 v[22:23], v[16:17], v[22:23], v[24:25] op_sel_hi:[1,0,1]
	v_pk_mul_f32 v[24:25], v[32:33], v[22:23] op_sel:[1,1] op_sel_hi:[1,0] neg_lo:[1,0]
	v_pk_fma_f32 v[24:25], v[32:33], v[22:23], v[24:25] op_sel_hi:[0,1,1]
	ds_write2_b64 v15, v[18:19], v[24:25] offset0:192 offset1:208
	v_pk_mul_f32 v[18:19], v[16:17], v[22:23] op_sel:[1,1] op_sel_hi:[0,1] neg_lo:[0,1]
	v_pk_fma_f32 v[18:19], v[16:17], v[22:23], v[18:19] op_sel_hi:[1,0,1]
	v_pk_mul_f32 v[22:23], v[20:21], v[18:19] op_sel:[1,1] op_sel_hi:[1,0] neg_lo:[1,0]
	v_pk_fma_f32 v[20:21], v[20:21], v[18:19], v[22:23] op_sel_hi:[0,1,1]
	v_pk_mul_f32 v[22:23], v[16:17], v[18:19] op_sel:[1,1] op_sel_hi:[0,1] neg_lo:[0,1]
	v_pk_fma_f32 v[16:17], v[16:17], v[18:19], v[22:23] op_sel_hi:[1,0,1]
	v_pk_mul_f32 v[18:19], v[36:37], v[16:17] op_sel:[1,1] op_sel_hi:[1,0] neg_lo:[1,0]
	v_pk_fma_f32 v[16:17], v[36:37], v[16:17], v[18:19] op_sel_hi:[0,1,1]
	ds_write2_b64 v13, v[20:21], v[16:17] offset0:224 offset1:240
	v_mov_b32_e32 v16, v1
	v_mov_b32_e32 v10, v178
	v_mov_b32_e32 v17, v177
	s_waitcnt lgkmcnt(0)
	s_barrier
	v_lshlrev_b32_e32 v190, 3, v16
	v_add_u32_e32 v190, 0x1000, v190
	global_load_dwordx2 v[196:197], v190, s[48:49] offset:-4096
	global_load_dwordx2 v[198:199], v190, s[48:49]
	v_add_u32_e32 v190, 0x2000, v190
	global_load_dwordx2 v[200:201], v190, s[48:49] offset:-4096
	global_load_dwordx2 v[202:203], v190, s[48:49]
	v_add_u32_e32 v190, 0x2000, v190
	global_load_dwordx2 v[204:205], v190, s[48:49] offset:-4096
	global_load_dwordx2 v[206:207], v190, s[48:49]
	v_add_u32_e32 v190, 0x2000, v190
	global_load_dwordx2 v[208:209], v190, s[48:49] offset:-4096
	global_load_dwordx2 v[210:211], v190, s[48:49]
	v_add_u32_e32 v190, 0x2000, v190
	global_load_dwordx2 v[212:213], v190, s[48:49] offset:-4096
	global_load_dwordx2 v[214:215], v190, s[48:49]
	v_add_u32_e32 v190, 0x2000, v190
	global_load_dwordx2 v[216:217], v190, s[48:49] offset:-4096
	global_load_dwordx2 v[218:219], v190, s[48:49]
	v_add_u32_e32 v190, 0x2000, v190
	global_load_dwordx2 v[220:221], v190, s[48:49] offset:-4096
	global_load_dwordx2 v[222:223], v190, s[48:49]
	v_add_u32_e32 v190, 0x2000, v190
	global_load_dwordx2 v[224:225], v190, s[48:49] offset:-4096
	global_load_dwordx2 v[226:227], v190, s[48:49]
	v_mov_b32_e32 v50, v166
	v_lshlrev_b32_e32 v13, 3, v17
	v_lshlrev_b32_e32 v48, 3, v10
	v_add3_u32 v10, 0, v13, v48
	v_xor_b32_e32 v13, 1, v17
	v_xor_b32_e32 v34, 8, v17
	v_xor_b32_e32 v36, 9, v17
	v_lshlrev_b32_e32 v13, 3, v13
	v_xor_b32_e32 v15, 2, v17
	v_xor_b32_e32 v24, 3, v17
	v_xor_b32_e32 v26, 4, v17
	v_xor_b32_e32 v28, 5, v17
	v_xor_b32_e32 v30, 6, v17
	v_xor_b32_e32 v32, 7, v17
	v_lshlrev_b32_e32 v34, 3, v34
	v_lshlrev_b32_e32 v36, 3, v36
	v_xor_b32_e32 v38, 10, v17
	v_xor_b32_e32 v40, 11, v17
	v_xor_b32_e32 v42, 12, v17
	v_xor_b32_e32 v44, 13, v17
	v_xor_b32_e32 v46, 14, v17
	v_xor_b32_e32 v17, 15, v17
	v_add3_u32 v13, 0, v13, v48
	v_lshlrev_b32_e32 v15, 3, v15
	v_lshlrev_b32_e32 v24, 3, v24
	v_lshlrev_b32_e32 v26, 3, v26
	v_lshlrev_b32_e32 v28, 3, v28
	v_lshlrev_b32_e32 v30, 3, v30
	v_lshlrev_b32_e32 v32, 3, v32
	v_add3_u32 v57, 0, v34, v48
	v_add3_u32 v58, 0, v36, v48
	v_lshlrev_b32_e32 v38, 3, v38
	v_lshlrev_b32_e32 v40, 3, v40
	v_lshlrev_b32_e32 v42, 3, v42
	v_lshlrev_b32_e32 v44, 3, v44
	v_lshlrev_b32_e32 v46, 3, v46
	v_lshlrev_b32_e32 v17, 3, v17
	ds_read_b64 v[18:19], v10
	ds_read_b64 v[20:21], v13
	v_add3_u32 v15, 0, v15, v48
	v_add3_u32 v52, 0, v24, v48
	v_add3_u32 v53, 0, v26, v48
	v_add3_u32 v54, 0, v28, v48
	v_add3_u32 v55, 0, v30, v48
	v_add3_u32 v56, 0, v32, v48
	ds_read_b64 v[34:35], v57
	ds_read_b64 v[36:37], v58
	v_add3_u32 v59, 0, v38, v48
	v_add3_u32 v60, 0, v40, v48
	v_add3_u32 v61, 0, v42, v48
	v_add3_u32 v62, 0, v44, v48
	v_add3_u32 v63, 0, v46, v48
	v_add3_u32 v64, 0, v17, v48
	v_mov_b32_e32 v17, v164
	ds_read_b64 v[22:23], v15
	ds_read_b64 v[24:25], v52
	ds_read_b64 v[26:27], v53
	ds_read_b64 v[28:29], v54
	ds_read_b64 v[30:31], v55
	ds_read_b64 v[32:33], v56
	ds_read_b64 v[38:39], v59
	ds_read_b64 v[40:41], v60
	ds_read_b64 v[42:43], v61
	ds_read_b64 v[44:45], v62
	ds_read_b64 v[46:47], v63
	ds_read_b64 v[48:49], v64
	s_waitcnt lgkmcnt(13)
	v_pk_add_f32 v[70:71], v[18:19], v[34:35]
	v_mov_b32_e32 v17, v165
	v_pk_add_f32 v[18:19], v[18:19], v[34:35] neg_lo:[0,1] neg_hi:[0,1]
	v_mov_b32_e32 v17, v167
	s_waitcnt lgkmcnt(12)
	v_pk_add_f32 v[34:35], v[20:21], v[36:37]
	v_pk_add_f32 v[20:21], v[20:21], v[36:37] neg_lo:[0,1] neg_hi:[0,1]
	v_mov_b32_e32 v66, v168
	v_mov_b32_e32 v17, v169
	v_mov_b32_e32 v68, v170
	s_nop 0
	v_pk_mul_f32 v[36:37], v[20:21], v[68:69] op_sel:[1,0] op_sel_hi:[0,0] neg_lo:[1,1] neg_hi:[0,1]
	v_mov_b32_e32 v17, v171
	v_pk_fma_f32 v[20:21], v[20:21], v[50:51], v[36:37] op_sel_hi:[1,0,1]
	s_waitcnt lgkmcnt(5)
	v_pk_add_f32 v[36:37], v[22:23], v[38:39]
	v_pk_add_f32 v[22:23], v[22:23], v[38:39] neg_lo:[0,1] neg_hi:[0,1]
	v_pk_mul_f32 v[38:39], v[22:23], v[66:67] op_sel:[1,0] op_sel_hi:[0,0] neg_lo:[1,1] neg_hi:[0,1]
	v_mov_b32_e32 v17, v172
	v_pk_fma_f32 v[22:23], v[22:23], v[66:67], v[38:39] op_sel_hi:[1,0,1]
	s_waitcnt lgkmcnt(4)
	v_pk_add_f32 v[38:39], v[24:25], v[40:41]
	v_pk_add_f32 v[24:25], v[24:25], v[40:41] neg_lo:[0,1] neg_hi:[0,1]
	v_pk_mul_f32 v[40:41], v[24:25], v[68:69] op_sel_hi:[1,0]
	v_pk_fma_f32 v[24:25], v[24:25], v[50:51], v[40:41] op_sel:[1,0,0] op_sel_hi:[0,0,1] neg_lo:[1,1,0] neg_hi:[0,1,0]
	s_waitcnt lgkmcnt(3)
	v_pk_add_f32 v[40:41], v[26:27], v[42:43]
	v_pk_add_f32 v[26:27], v[26:27], v[42:43] neg_lo:[0,1] neg_hi:[0,1]
	v_ashrrev_i32_e32 v17, 31, v16
	v_xor_b32_e32 v73, 0x80000000, v26
	v_mov_b32_e32 v72, v27
	s_waitcnt lgkmcnt(2)
	v_pk_add_f32 v[26:27], v[28:29], v[44:45]
	v_pk_add_f32 v[28:29], v[28:29], v[44:45] neg_lo:[0,1] neg_hi:[0,1]
	v_pk_mul_f32 v[42:43], v[28:29], v[68:69] op_sel_hi:[1,0] neg_lo:[0,1] neg_hi:[0,1]
	v_pk_fma_f32 v[28:29], v[28:29], v[50:51], v[42:43] op_sel:[1,0,0] op_sel_hi:[0,0,1] neg_lo:[1,1,0] neg_hi:[0,1,0]
	s_waitcnt lgkmcnt(1)
	v_pk_add_f32 v[42:43], v[30:31], v[46:47]
	v_pk_add_f32 v[30:31], v[30:31], v[46:47] neg_lo:[0,1] neg_hi:[0,1]
	v_pk_mul_f32 v[44:45], v[30:31], v[66:67] op_sel:[1,0] op_sel_hi:[0,0] neg_lo:[1,1] neg_hi:[0,1]
	v_pk_fma_f32 v[30:31], v[30:31], v[66:67], v[44:45] op_sel_hi:[1,0,1] neg_lo:[0,1,0] neg_hi:[0,1,0]
	s_waitcnt lgkmcnt(0)
	v_pk_add_f32 v[44:45], v[32:33], v[48:49]
	v_pk_add_f32 v[32:33], v[32:33], v[48:49] neg_lo:[0,1] neg_hi:[0,1]
	v_pk_add_f32 v[48:49], v[34:35], v[26:27]
	v_pk_add_f32 v[26:27], v[34:35], v[26:27] neg_lo:[0,1] neg_hi:[0,1]
	v_pk_mul_f32 v[34:35], v[26:27], v[66:67] op_sel:[1,0] op_sel_hi:[0,0] neg_lo:[1,1] neg_hi:[0,1]
	v_pk_fma_f32 v[26:27], v[26:27], v[66:67], v[34:35] op_sel_hi:[1,0,1]
	v_pk_add_f32 v[34:35], v[36:37], v[42:43]
	v_pk_add_f32 v[36:37], v[36:37], v[42:43] neg_lo:[0,1] neg_hi:[0,1]
	v_pk_mul_f32 v[46:47], v[32:33], v[68:69] op_sel:[1,0] op_sel_hi:[0,0] neg_lo:[1,1] neg_hi:[0,1]
	v_xor_b32_e32 v43, 0x80000000, v36
	v_mov_b32_e32 v42, v37
	v_pk_add_f32 v[36:37], v[38:39], v[44:45]
	v_pk_add_f32 v[38:39], v[38:39], v[44:45] neg_lo:[0,1] neg_hi:[0,1]
	v_pk_fma_f32 v[46:47], v[32:33], v[50:51], v[46:47] op_sel_hi:[1,0,1] neg_lo:[0,1,0] neg_hi:[0,1,0]
	v_pk_add_f32 v[32:33], v[70:71], v[40:41]
	v_pk_mul_f32 v[44:45], v[38:39], v[66:67] op_sel:[1,0] op_sel_hi:[0,0] neg_lo:[1,1] neg_hi:[0,1]
	v_pk_add_f32 v[40:41], v[70:71], v[40:41] neg_lo:[0,1] neg_hi:[0,1]
	v_pk_fma_f32 v[38:39], v[38:39], v[66:67], v[44:45] op_sel_hi:[1,0,1] neg_lo:[0,1,0] neg_hi:[0,1,0]
	v_pk_add_f32 v[44:45], v[32:33], v[34:35]
	v_pk_add_f32 v[32:33], v[32:33], v[34:35] neg_lo:[0,1] neg_hi:[0,1]
	v_pk_add_f32 v[34:35], v[48:49], v[36:37]
	v_pk_add_f32 v[36:37], v[48:49], v[36:37] neg_lo:[0,1] neg_hi:[0,1]
	v_pk_add_f32 v[50:51], v[44:45], v[34:35]
	v_xor_b32_e32 v49, 0x80000000, v36
	v_mov_b32_e32 v48, v37
	v_pk_add_f32 v[36:37], v[44:45], v[34:35] neg_lo:[0,1] neg_hi:[0,1]
	v_pk_add_f32 v[68:69], v[32:33], v[48:49]
	v_pk_add_f32 v[44:45], v[32:33], v[48:49] neg_lo:[0,1] neg_hi:[0,1]
	v_pk_add_f32 v[32:33], v[40:41], v[42:43]
	v_pk_add_f32 v[34:35], v[40:41], v[42:43] neg_lo:[0,1] neg_hi:[0,1]
	v_pk_add_f32 v[40:41], v[26:27], v[38:39]
	v_pk_add_f32 v[26:27], v[26:27], v[38:39] neg_lo:[0,1] neg_hi:[0,1]
	v_pk_add_f32 v[42:43], v[32:33], v[40:41] neg_lo:[0,1] neg_hi:[0,1]
	v_xor_b32_e32 v39, 0x80000000, v26
	v_mov_b32_e32 v38, v27
	v_pk_add_f32 v[26:27], v[32:33], v[40:41]
	v_pk_add_f32 v[40:41], v[20:21], v[28:29]
	v_pk_add_f32 v[20:21], v[20:21], v[28:29] neg_lo:[0,1] neg_hi:[0,1]
	v_pk_add_f32 v[32:33], v[34:35], v[38:39]
	v_pk_mul_f32 v[28:29], v[66:67], v[20:21] op_sel:[0,1] op_sel_hi:[0,0] neg_lo:[1,1] neg_hi:[1,0]
	v_pk_fma_f32 v[20:21], v[66:67], v[20:21], v[28:29] op_sel_hi:[0,1,1]
	v_pk_add_f32 v[28:29], v[22:23], v[30:31]
	v_pk_add_f32 v[22:23], v[22:23], v[30:31] neg_lo:[0,1] neg_hi:[0,1]
	v_pk_add_f32 v[38:39], v[34:35], v[38:39] neg_lo:[0,1] neg_hi:[0,1]
	v_xor_b32_e32 v31, 0x80000000, v22
	v_mov_b32_e32 v30, v23
	v_pk_add_f32 v[22:23], v[24:25], v[46:47]
	v_pk_add_f32 v[24:25], v[24:25], v[46:47] neg_lo:[0,1] neg_hi:[0,1]
	v_pk_add_f32 v[34:35], v[18:19], v[72:73]
	v_pk_mul_f32 v[46:47], v[66:67], v[24:25] op_sel:[0,1] op_sel_hi:[0,0] neg_lo:[1,1] neg_hi:[1,0]
	v_pk_fma_f32 v[24:25], v[66:67], v[24:25], v[46:47] op_sel_hi:[0,1,1] neg_lo:[1,0,0] neg_hi:[1,0,0]
	v_pk_add_f32 v[46:47], v[34:35], v[28:29]
	v_pk_add_f32 v[28:29], v[34:35], v[28:29] neg_lo:[0,1] neg_hi:[0,1]
	v_pk_add_f32 v[34:35], v[40:41], v[22:23]
	v_pk_add_f32 v[22:23], v[40:41], v[22:23] neg_lo:[0,1] neg_hi:[0,1]
	v_pk_add_f32 v[18:19], v[18:19], v[72:73] neg_lo:[0,1] neg_hi:[0,1]
	v_pk_add_f32 v[66:67], v[28:29], v[22:23] op_sel:[0,1] op_sel_hi:[1,0] neg_hi:[0,1]
	v_pk_add_f32 v[48:49], v[28:29], v[22:23] op_sel:[0,1] op_sel_hi:[1,0] neg_lo:[0,1]
	v_pk_add_f32 v[28:29], v[18:19], v[30:31]
	v_pk_add_f32 v[18:19], v[18:19], v[30:31] neg_lo:[0,1] neg_hi:[0,1]
	v_pk_add_f32 v[30:31], v[20:21], v[24:25]
	v_pk_add_f32 v[20:21], v[20:21], v[24:25] neg_lo:[0,1] neg_hi:[0,1]
	v_pk_add_f32 v[22:23], v[46:47], v[34:35]
	v_xor_b32_e32 v25, 0x80000000, v20
	v_mov_b32_e32 v24, v21
	v_lshl_add_u64 v[20:21], v[16:17], 3, s[48:49]
	s_waitcnt vmcnt(0)
	v_pk_add_f32 v[40:41], v[46:47], v[34:35] neg_lo:[0,1] neg_hi:[0,1]
	v_pk_add_f32 v[34:35], v[18:19], v[24:25]
	v_pk_add_f32 v[18:19], v[18:19], v[24:25] neg_lo:[0,1] neg_hi:[0,1]
	v_pk_add_f32 v[70:71], v[28:29], v[30:31]
	v_pk_add_f32 v[46:47], v[28:29], v[30:31] neg_lo:[0,1] neg_hi:[0,1]
	v_mov_b32_e32 v17, v164
	s_nop 0
	v_pk_mul_f32 v[24:25], v[50:51], v[196:197] op_sel:[1,1] op_sel_hi:[1,0] neg_lo:[1,0]
	v_pk_fma_f32 v[20:21], v[50:51], v[196:197], v[24:25] op_sel_hi:[0,1,1]
	v_add_u32_e32 v24, 0x200, v16
	v_ashrrev_i32_e32 v25, 31, v24
	v_lshl_add_u64 v[24:25], v[24:25], 3, s[48:49]
	s_nop 0
	v_pk_mul_f32 v[28:29], v[198:199], v[22:23] op_sel:[1,1] op_sel_hi:[0,1] neg_lo:[0,1]
	v_pk_fma_f32 v[22:23], v[198:199], v[22:23], v[28:29] op_sel_hi:[1,0,1]
	v_add_u32_e32 v24, 0x400, v16
	v_ashrrev_i32_e32 v25, 31, v24
	v_lshl_add_u64 v[24:25], v[24:25], 3, s[48:49]
	s_nop 0
	v_pk_mul_f32 v[28:29], v[26:27], v[200:201] op_sel:[1,1] op_sel_hi:[1,0] neg_lo:[1,0]
	v_pk_fma_f32 v[24:25], v[26:27], v[200:201], v[28:29] op_sel_hi:[0,1,1]
	v_add_u32_e32 v26, 0x600, v16
	v_ashrrev_i32_e32 v27, 31, v26
	v_lshl_add_u64 v[26:27], v[26:27], 3, s[48:49]
	s_nop 0
	v_pk_mul_f32 v[28:29], v[202:203], v[70:71] op_sel:[1,1] op_sel_hi:[0,1] neg_lo:[0,1]
	v_pk_fma_f32 v[26:27], v[202:203], v[70:71], v[28:29] op_sel_hi:[1,0,1]
	v_add_u32_e32 v28, 0x800, v16
	v_ashrrev_i32_e32 v29, 31, v28
	v_lshl_add_u64 v[28:29], v[28:29], 3, s[48:49]
	s_nop 0
	v_pk_mul_f32 v[30:31], v[68:69], v[204:205] op_sel:[1,1] op_sel_hi:[1,0] neg_lo:[1,0]
	v_pk_fma_f32 v[28:29], v[68:69], v[204:205], v[30:31] op_sel_hi:[0,1,1]
	v_add_u32_e32 v30, 0xa00, v16
	v_ashrrev_i32_e32 v31, 31, v30
	v_lshl_add_u64 v[30:31], v[30:31], 3, s[48:49]
	v_mov_b32_e32 v68, v170
	s_nop 0
	v_pk_mul_f32 v[50:51], v[206:207], v[66:67] op_sel:[1,1] op_sel_hi:[0,1] neg_lo:[0,1]
	v_pk_fma_f32 v[30:31], v[206:207], v[66:67], v[50:51] op_sel_hi:[1,0,1]
	v_add_u32_e32 v50, 0xc00, v16
	v_ashrrev_i32_e32 v51, 31, v50
	v_lshl_add_u64 v[50:51], v[50:51], 3, s[48:49]
	s_nop 0
	v_pk_mul_f32 v[66:67], v[32:33], v[208:209] op_sel:[1,1] op_sel_hi:[1,0] neg_lo:[1,0]
	v_pk_fma_f32 v[32:33], v[32:33], v[208:209], v[66:67] op_sel_hi:[0,1,1]
	v_add_u32_e32 v50, 0xe00, v16
	v_ashrrev_i32_e32 v51, 31, v50
	v_lshl_add_u64 v[50:51], v[50:51], 3, s[48:49]
	s_nop 0
	v_pk_mul_f32 v[66:67], v[210:211], v[34:35] op_sel:[1,1] op_sel_hi:[0,1] neg_lo:[0,1]
	v_pk_fma_f32 v[34:35], v[210:211], v[34:35], v[66:67] op_sel_hi:[1,0,1]
	v_add_u32_e32 v50, 0x1000, v16
	v_ashrrev_i32_e32 v51, 31, v50
	v_lshl_add_u64 v[50:51], v[50:51], 3, s[48:49]
	s_nop 0
	v_pk_mul_f32 v[66:67], v[36:37], v[212:213] op_sel:[1,1] op_sel_hi:[1,0] neg_lo:[1,0]
	v_pk_fma_f32 v[36:37], v[36:37], v[212:213], v[66:67] op_sel_hi:[0,1,1]
	v_add_u32_e32 v50, 0x1200, v16
	v_ashrrev_i32_e32 v51, 31, v50
	v_lshl_add_u64 v[50:51], v[50:51], 3, s[48:49]
	v_pk_add_f32 v[70:71], v[20:21], v[36:37]
	v_pk_add_f32 v[20:21], v[20:21], v[36:37] neg_lo:[0,1] neg_hi:[0,1]
	s_nop 0
	v_pk_mul_f32 v[66:67], v[40:41], v[214:215] op_sel:[1,1] op_sel_hi:[1,0] neg_lo:[1,0]
	v_pk_fma_f32 v[40:41], v[40:41], v[214:215], v[66:67] op_sel_hi:[0,1,1]
	v_add_u32_e32 v50, 0x1400, v16
	v_ashrrev_i32_e32 v51, 31, v50
	v_lshl_add_u64 v[50:51], v[50:51], 3, s[48:49]
	v_pk_add_f32 v[36:37], v[22:23], v[40:41]
	v_pk_add_f32 v[22:23], v[22:23], v[40:41] neg_lo:[0,1] neg_hi:[0,1]
	s_nop 0
	v_pk_mul_f32 v[66:67], v[42:43], v[216:217] op_sel:[1,1] op_sel_hi:[1,0] neg_lo:[1,0]
	v_pk_fma_f32 v[42:43], v[42:43], v[216:217], v[66:67] op_sel_hi:[0,1,1]
	v_add_u32_e32 v50, 0x1600, v16
	v_ashrrev_i32_e32 v51, 31, v50
	v_lshl_add_u64 v[50:51], v[50:51], 3, s[48:49]
	s_nop 0
	v_pk_mul_f32 v[66:67], v[46:47], v[218:219] op_sel:[1,1] op_sel_hi:[1,0] neg_lo:[1,0]
	v_pk_fma_f32 v[46:47], v[46:47], v[218:219], v[66:67] op_sel_hi:[0,1,1]
	v_add_u32_e32 v50, 0x1800, v16
	v_ashrrev_i32_e32 v51, 31, v50
	v_lshl_add_u64 v[50:51], v[50:51], 3, s[48:49]
	s_nop 0
	v_pk_mul_f32 v[66:67], v[44:45], v[220:221] op_sel:[1,1] op_sel_hi:[1,0] neg_lo:[1,0]
	v_pk_fma_f32 v[44:45], v[44:45], v[220:221], v[66:67] op_sel_hi:[0,1,1]
	v_add_u32_e32 v50, 0x1a00, v16
	v_ashrrev_i32_e32 v51, 31, v50
	v_lshl_add_u64 v[50:51], v[50:51], 3, s[48:49]
	s_nop 0
	v_pk_mul_f32 v[66:67], v[48:49], v[222:223] op_sel:[1,1] op_sel_hi:[1,0] neg_lo:[1,0]
	v_pk_fma_f32 v[48:49], v[48:49], v[222:223], v[66:67] op_sel_hi:[0,1,1]
	v_add_u32_e32 v50, 0x1c00, v16
	v_ashrrev_i32_e32 v51, 31, v50
	v_lshl_add_u64 v[50:51], v[50:51], 3, s[48:49]
	s_nop 0
	v_pk_mul_f32 v[66:67], v[38:39], v[224:225] op_sel:[1,1] op_sel_hi:[1,0] neg_lo:[1,0]
	v_pk_fma_f32 v[38:39], v[38:39], v[224:225], v[66:67] op_sel_hi:[0,1,1]
	v_add_u32_e32 v50, 0x1e00, v16
	v_ashrrev_i32_e32 v51, 31, v50
	v_lshl_add_u64 v[50:51], v[50:51], 3, s[48:49]
	v_mov_b32_e32 v50, v226
	v_mov_b32_e32 v51, v227
	v_lshlrev_b32_e32 v190, 3, v16
	v_add_u32_e32 v190, 0x11000, v190
	global_load_dwordx2 v[196:197], v190, s[48:49] offset:-4096
	global_load_dwordx2 v[198:199], v190, s[48:49]
	v_add_u32_e32 v190, 0x2000, v190
	global_load_dwordx2 v[200:201], v190, s[48:49] offset:-4096
	global_load_dwordx2 v[202:203], v190, s[48:49]
	v_add_u32_e32 v190, 0x2000, v190
	global_load_dwordx2 v[204:205], v190, s[48:49] offset:-4096
	global_load_dwordx2 v[206:207], v190, s[48:49]
	v_add_u32_e32 v190, 0x2000, v190
	global_load_dwordx2 v[208:209], v190, s[48:49] offset:-4096
	global_load_dwordx2 v[210:211], v190, s[48:49]
	v_add_u32_e32 v190, 0x2000, v190
	global_load_dwordx2 v[212:213], v190, s[48:49] offset:-4096
	global_load_dwordx2 v[214:215], v190, s[48:49]
	v_add_u32_e32 v190, 0x2000, v190
	global_load_dwordx2 v[216:217], v190, s[48:49] offset:-4096
	global_load_dwordx2 v[218:219], v190, s[48:49]
	v_add_u32_e32 v190, 0x2000, v190
	global_load_dwordx2 v[220:221], v190, s[48:49] offset:-4096
	global_load_dwordx2 v[222:223], v190, s[48:49]
	v_add_u32_e32 v190, 0x2000, v190
	global_load_dwordx2 v[224:225], v190, s[48:49] offset:-4096
	global_load_dwordx2 v[226:227], v190, s[48:49]
	v_mov_b32_e32 v17, v165
	s_nop 0
	v_pk_mul_f32 v[66:67], v[18:19], v[50:51] op_sel:[1,1] op_sel_hi:[1,0] neg_lo:[1,0]
	v_pk_fma_f32 v[18:19], v[18:19], v[50:51], v[66:67] op_sel_hi:[0,1,1]
	v_mov_b32_e32 v50, v166
	v_mov_b32_e32 v17, v167
	v_mov_b32_e32 v66, v168
	v_mov_b32_e32 v17, v169
	s_nop 0
	v_pk_mul_f32 v[40:41], v[22:23], v[68:69] op_sel:[1,0] op_sel_hi:[0,0] neg_lo:[1,0]
	v_mov_b32_e32 v17, v171
	v_pk_fma_f32 v[22:23], v[22:23], v[50:51], v[40:41] op_sel_hi:[1,0,1]
	v_pk_add_f32 v[40:41], v[24:25], v[42:43]
	v_pk_add_f32 v[24:25], v[24:25], v[42:43] neg_lo:[0,1] neg_hi:[0,1]
	v_pk_mul_f32 v[42:43], v[24:25], v[66:67] op_sel:[1,0] op_sel_hi:[0,0] neg_lo:[1,0]
	v_mov_b32_e32 v17, v172
	v_pk_fma_f32 v[24:25], v[24:25], v[66:67], v[42:43] op_sel_hi:[1,0,1]
	v_pk_add_f32 v[42:43], v[26:27], v[46:47]
	v_pk_add_f32 v[26:27], v[26:27], v[46:47] neg_lo:[0,1] neg_hi:[0,1]
	v_pk_mul_f32 v[46:47], v[26:27], v[68:69] op_sel_hi:[1,0]
	v_pk_fma_f32 v[26:27], v[26:27], v[50:51], v[46:47] op_sel:[1,0,0] op_sel_hi:[0,0,1] neg_lo:[1,0,0]
	v_pk_add_f32 v[46:47], v[28:29], v[44:45]
	v_pk_add_f32 v[28:29], v[28:29], v[44:45] neg_lo:[0,1] neg_hi:[0,1]
	v_mov_b32_e32 v17, v177
	v_xor_b32_e32 v44, 0x80000000, v29
	v_mov_b32_e32 v45, v28
	v_pk_add_f32 v[28:29], v[30:31], v[48:49]
	v_pk_add_f32 v[30:31], v[30:31], v[48:49] neg_lo:[0,1] neg_hi:[0,1]
	v_pk_mul_f32 v[48:49], v[30:31], v[68:69] op_sel_hi:[1,0] neg_lo:[0,1] neg_hi:[0,1]
	v_pk_fma_f32 v[30:31], v[30:31], v[50:51], v[48:49] op_sel:[1,0,0] op_sel_hi:[0,0,1] neg_lo:[1,0,0]
	v_pk_add_f32 v[48:49], v[32:33], v[38:39]
	v_pk_add_f32 v[32:33], v[32:33], v[38:39] neg_lo:[0,1] neg_hi:[0,1]
	v_pk_mul_f32 v[38:39], v[32:33], v[66:67] op_sel:[1,0] op_sel_hi:[0,0] neg_lo:[1,0]
	v_pk_fma_f32 v[32:33], v[32:33], v[66:67], v[38:39] op_sel_hi:[1,0,1] neg_lo:[0,1,0] neg_hi:[0,1,0]
	v_pk_add_f32 v[38:39], v[34:35], v[18:19]
	v_pk_add_f32 v[18:19], v[34:35], v[18:19] neg_lo:[0,1] neg_hi:[0,1]
	v_pk_mul_f32 v[34:35], v[18:19], v[68:69] op_sel:[1,0] op_sel_hi:[0,0] neg_lo:[1,0]
	v_mov_b32_e32 v68, v170
	v_pk_fma_f32 v[18:19], v[18:19], v[50:51], v[34:35] op_sel_hi:[1,0,1] neg_lo:[0,1,0] neg_hi:[0,1,0]
	v_pk_add_f32 v[50:51], v[36:37], v[28:29]
	v_pk_add_f32 v[28:29], v[36:37], v[28:29] neg_lo:[0,1] neg_hi:[0,1]
	v_pk_add_f32 v[34:35], v[70:71], v[46:47]
	v_pk_mul_f32 v[36:37], v[28:29], v[66:67] op_sel:[1,0] op_sel_hi:[0,0] neg_lo:[1,0]
	v_pk_add_f32 v[46:47], v[70:71], v[46:47] neg_lo:[0,1] neg_hi:[0,1]
	v_pk_fma_f32 v[28:29], v[28:29], v[66:67], v[36:37] op_sel_hi:[1,0,1]
	v_pk_add_f32 v[36:37], v[40:41], v[48:49]
	v_pk_add_f32 v[40:41], v[40:41], v[48:49] neg_lo:[0,1] neg_hi:[0,1]
	v_xor_b32_e32 v48, 0x80000000, v41
	v_mov_b32_e32 v49, v40
	v_pk_add_f32 v[40:41], v[42:43], v[38:39]
	v_pk_add_f32 v[38:39], v[42:43], v[38:39] neg_lo:[0,1] neg_hi:[0,1]
	v_pk_mul_f32 v[42:43], v[66:67], v[38:39] op_sel:[0,1] op_sel_hi:[0,0] neg_lo:[0,1]
	v_pk_fma_f32 v[38:39], v[38:39], v[66:67], v[42:43] op_sel_hi:[1,0,1] neg_lo:[0,1,0] neg_hi:[0,1,0]
	v_pk_add_f32 v[42:43], v[34:35], v[36:37]
	v_pk_add_f32 v[34:35], v[34:35], v[36:37] neg_lo:[0,1] neg_hi:[0,1]
	v_pk_add_f32 v[36:37], v[50:51], v[40:41]
	v_pk_add_f32 v[40:41], v[50:51], v[40:41] neg_lo:[0,1] neg_hi:[0,1]
	v_xor_b32_e32 v50, 0x80000000, v41
	v_mov_b32_e32 v51, v40
	v_pk_add_f32 v[40:41], v[42:43], v[36:37]
	v_pk_add_f32 v[36:37], v[42:43], v[36:37] neg_lo:[0,1] neg_hi:[0,1]
	v_pk_add_f32 v[42:43], v[34:35], v[50:51]
	v_pk_add_f32 v[34:35], v[34:35], v[50:51] neg_lo:[0,1] neg_hi:[0,1]
	v_pk_add_f32 v[50:51], v[46:47], v[48:49]
	v_pk_add_f32 v[46:47], v[46:47], v[48:49] neg_lo:[0,1] neg_hi:[0,1]
	v_pk_add_f32 v[48:49], v[28:29], v[38:39]
	v_pk_add_f32 v[28:29], v[28:29], v[38:39] neg_lo:[0,1] neg_hi:[0,1]
	v_xor_b32_e32 v38, 0x80000000, v29
	v_mov_b32_e32 v39, v28
	v_pk_add_f32 v[28:29], v[50:51], v[48:49]
	v_pk_add_f32 v[48:49], v[50:51], v[48:49] neg_lo:[0,1] neg_hi:[0,1]
	v_pk_add_f32 v[50:51], v[46:47], v[38:39]
	v_pk_add_f32 v[38:39], v[46:47], v[38:39] neg_lo:[0,1] neg_hi:[0,1]
	v_pk_add_f32 v[46:47], v[20:21], v[44:45]
	v_pk_add_f32 v[20:21], v[20:21], v[44:45] neg_lo:[0,1] neg_hi:[0,1]
	v_pk_add_f32 v[44:45], v[22:23], v[30:31]
	v_pk_add_f32 v[22:23], v[22:23], v[30:31] neg_lo:[0,1] neg_hi:[0,1]
	v_pk_mul_f32 v[30:31], v[66:67], v[22:23] op_sel:[0,1] op_sel_hi:[0,0] neg_lo:[0,1]
	v_pk_fma_f32 v[22:23], v[66:67], v[22:23], v[30:31] op_sel_hi:[0,1,1]
	v_pk_add_f32 v[30:31], v[24:25], v[32:33]
	v_pk_add_f32 v[24:25], v[24:25], v[32:33] neg_lo:[0,1] neg_hi:[0,1]
	v_xor_b32_e32 v32, 0x80000000, v25
	v_mov_b32_e32 v33, v24
	v_pk_add_f32 v[24:25], v[26:27], v[18:19]
	v_pk_add_f32 v[18:19], v[26:27], v[18:19] neg_lo:[0,1] neg_hi:[0,1]
	v_pk_mul_f32 v[26:27], v[66:67], v[18:19] op_sel:[0,1] op_sel_hi:[0,0] neg_lo:[0,1]
	v_pk_fma_f32 v[18:19], v[66:67], v[18:19], v[26:27] op_sel_hi:[0,1,1] neg_lo:[1,0,0] neg_hi:[1,0,0]
	v_pk_add_f32 v[26:27], v[46:47], v[30:31]
	v_pk_add_f32 v[30:31], v[46:47], v[30:31] neg_lo:[0,1] neg_hi:[0,1]
	v_pk_add_f32 v[46:47], v[44:45], v[24:25]
	v_pk_add_f32 v[24:25], v[44:45], v[24:25] neg_lo:[0,1] neg_hi:[0,1]
	v_mov_b32_e32 v66, v168
	v_xor_b32_e32 v44, 0x80000000, v25
	v_mov_b32_e32 v45, v24
	v_pk_add_f32 v[24:25], v[26:27], v[46:47]
	v_pk_add_f32 v[26:27], v[26:27], v[46:47] neg_lo:[0,1] neg_hi:[0,1]
	v_pk_add_f32 v[46:47], v[30:31], v[44:45]
	v_pk_add_f32 v[30:31], v[30:31], v[44:45] neg_lo:[0,1] neg_hi:[0,1]
	v_pk_add_f32 v[44:45], v[20:21], v[32:33]
	v_pk_add_f32 v[20:21], v[20:21], v[32:33] neg_lo:[0,1] neg_hi:[0,1]
	v_pk_add_f32 v[32:33], v[22:23], v[18:19]
	v_pk_add_f32 v[18:19], v[22:23], v[18:19] neg_lo:[0,1] neg_hi:[0,1]
	v_xor_b32_e32 v22, 0x80000000, v19
	v_mov_b32_e32 v23, v18
	v_pk_add_f32 v[18:19], v[44:45], v[32:33]
	v_pk_add_f32 v[32:33], v[44:45], v[32:33] neg_lo:[0,1] neg_hi:[0,1]
	v_pk_add_f32 v[44:45], v[20:21], v[22:23]
	v_pk_add_f32 v[20:21], v[20:21], v[22:23] neg_lo:[0,1] neg_hi:[0,1]
	ds_write_b64 v10, v[40:41]
	ds_write_b64 v13, v[24:25]
	ds_write_b64 v15, v[28:29]
	ds_write_b64 v52, v[18:19]
	ds_write_b64 v53, v[42:43]
	ds_write_b64 v54, v[46:47]
	ds_write_b64 v55, v[50:51]
	ds_write_b64 v56, v[44:45]
	ds_write_b64 v57, v[36:37]
	ds_write_b64 v58, v[26:27]
	ds_write_b64 v59, v[48:49]
	ds_write_b64 v60, v[32:33]
	ds_write_b64 v61, v[34:35]
	ds_write_b64 v62, v[30:31]
	ds_write_b64 v63, v[38:39]
	ds_write_b64 v64, v[20:21]
	v_mov_b32_e32 v10, v179
	v_mov_b32_e32 v64, v166
	v_lshlrev_b32_e32 v13, 3, v17
	v_lshlrev_b32_e32 v48, 3, v10
	v_add3_u32 v10, 0, v13, v48
	v_xor_b32_e32 v13, 1, v17
	v_xor_b32_e32 v34, 8, v17
	v_xor_b32_e32 v36, 9, v17
	v_lshlrev_b32_e32 v13, 3, v13
	v_xor_b32_e32 v15, 2, v17
	v_xor_b32_e32 v24, 3, v17
	v_xor_b32_e32 v26, 4, v17
	v_xor_b32_e32 v28, 5, v17
	v_xor_b32_e32 v30, 6, v17
	v_xor_b32_e32 v32, 7, v17
	v_lshlrev_b32_e32 v34, 3, v34
	v_lshlrev_b32_e32 v36, 3, v36
	v_xor_b32_e32 v38, 10, v17
	v_xor_b32_e32 v40, 11, v17
	v_xor_b32_e32 v42, 12, v17
	v_xor_b32_e32 v44, 13, v17
	v_xor_b32_e32 v46, 14, v17
	v_xor_b32_e32 v17, 15, v17
	v_add3_u32 v13, 0, v13, v48
	v_lshlrev_b32_e32 v15, 3, v15
	v_lshlrev_b32_e32 v24, 3, v24
	v_lshlrev_b32_e32 v26, 3, v26
	v_lshlrev_b32_e32 v28, 3, v28
	v_lshlrev_b32_e32 v30, 3, v30
	v_lshlrev_b32_e32 v32, 3, v32
	v_add3_u32 v55, 0, v34, v48
	v_add3_u32 v56, 0, v36, v48
	v_lshlrev_b32_e32 v38, 3, v38
	v_lshlrev_b32_e32 v40, 3, v40
	v_lshlrev_b32_e32 v42, 3, v42
	v_lshlrev_b32_e32 v44, 3, v44
	v_lshlrev_b32_e32 v46, 3, v46
	v_lshlrev_b32_e32 v17, 3, v17
	ds_read_b64 v[18:19], v10
	ds_read_b64 v[20:21], v13
	v_add3_u32 v15, 0, v15, v48
	v_add3_u32 v50, 0, v24, v48
	v_add3_u32 v51, 0, v26, v48
	v_add3_u32 v52, 0, v28, v48
	v_add3_u32 v53, 0, v30, v48
	v_add3_u32 v54, 0, v32, v48
	ds_read_b64 v[34:35], v55
	ds_read_b64 v[36:37], v56
	v_add3_u32 v57, 0, v38, v48
	v_add3_u32 v58, 0, v40, v48
	v_add3_u32 v59, 0, v42, v48
	v_add3_u32 v60, 0, v44, v48
	v_add3_u32 v61, 0, v46, v48
	v_add3_u32 v62, 0, v17, v48
	v_mov_b32_e32 v17, v164
	ds_read_b64 v[22:23], v15
	ds_read_b64 v[24:25], v50
	ds_read_b64 v[26:27], v51
	ds_read_b64 v[28:29], v52
	ds_read_b64 v[30:31], v53
	ds_read_b64 v[32:33], v54
	ds_read_b64 v[38:39], v57
	ds_read_b64 v[40:41], v58
	ds_read_b64 v[42:43], v59
	ds_read_b64 v[44:45], v60
	ds_read_b64 v[46:47], v61
	ds_read_b64 v[48:49], v62
	s_waitcnt lgkmcnt(13)
	v_pk_add_f32 v[70:71], v[18:19], v[34:35]
	v_mov_b32_e32 v17, v165
	v_pk_add_f32 v[18:19], v[18:19], v[34:35] neg_lo:[0,1] neg_hi:[0,1]
	v_mov_b32_e32 v17, v167
	s_waitcnt lgkmcnt(12)
	v_pk_add_f32 v[34:35], v[20:21], v[36:37]
	v_pk_add_f32 v[20:21], v[20:21], v[36:37] neg_lo:[0,1] neg_hi:[0,1]
	v_mov_b32_e32 v17, v169
	s_nop 0
	v_pk_mul_f32 v[36:37], v[20:21], v[68:69] op_sel:[1,0] op_sel_hi:[0,0] neg_lo:[1,1] neg_hi:[0,1]
	v_mov_b32_e32 v17, v171
	v_pk_fma_f32 v[20:21], v[20:21], v[64:65], v[36:37] op_sel_hi:[1,0,1]
	s_waitcnt lgkmcnt(5)
	v_pk_add_f32 v[36:37], v[22:23], v[38:39]
	v_pk_add_f32 v[22:23], v[22:23], v[38:39] neg_lo:[0,1] neg_hi:[0,1]
	v_pk_mul_f32 v[38:39], v[22:23], v[66:67] op_sel:[1,0] op_sel_hi:[0,0] neg_lo:[1,1] neg_hi:[0,1]
	v_mov_b32_e32 v17, v172
	v_pk_fma_f32 v[22:23], v[22:23], v[66:67], v[38:39] op_sel_hi:[1,0,1]
	s_waitcnt lgkmcnt(4)
	v_pk_add_f32 v[38:39], v[24:25], v[40:41]
	v_pk_add_f32 v[24:25], v[24:25], v[40:41] neg_lo:[0,1] neg_hi:[0,1]
	v_pk_mul_f32 v[40:41], v[24:25], v[68:69] op_sel_hi:[1,0]
	v_pk_fma_f32 v[24:25], v[24:25], v[64:65], v[40:41] op_sel:[1,0,0] op_sel_hi:[0,0,1] neg_lo:[1,1,0] neg_hi:[0,1,0]
	s_waitcnt lgkmcnt(3)
	v_pk_add_f32 v[40:41], v[26:27], v[42:43]
	v_pk_add_f32 v[26:27], v[26:27], v[42:43] neg_lo:[0,1] neg_hi:[0,1]
	v_xor_b32_e32 v73, 0x80000000, v26
	v_mov_b32_e32 v72, v27
	s_waitcnt lgkmcnt(2)
	v_pk_add_f32 v[26:27], v[28:29], v[44:45]
	v_pk_add_f32 v[28:29], v[28:29], v[44:45] neg_lo:[0,1] neg_hi:[0,1]
	v_pk_mul_f32 v[42:43], v[28:29], v[68:69] op_sel_hi:[1,0] neg_lo:[0,1] neg_hi:[0,1]
	v_pk_fma_f32 v[28:29], v[28:29], v[64:65], v[42:43] op_sel:[1,0,0] op_sel_hi:[0,0,1] neg_lo:[1,1,0] neg_hi:[0,1,0]
	s_waitcnt lgkmcnt(1)
	v_pk_add_f32 v[42:43], v[30:31], v[46:47]
	v_pk_add_f32 v[30:31], v[30:31], v[46:47] neg_lo:[0,1] neg_hi:[0,1]
	v_pk_mul_f32 v[44:45], v[30:31], v[66:67] op_sel:[1,0] op_sel_hi:[0,0] neg_lo:[1,1] neg_hi:[0,1]
	v_pk_fma_f32 v[30:31], v[30:31], v[66:67], v[44:45] op_sel_hi:[1,0,1] neg_lo:[0,1,0] neg_hi:[0,1,0]
	s_waitcnt lgkmcnt(0)
	v_pk_add_f32 v[44:45], v[32:33], v[48:49]
	v_pk_add_f32 v[32:33], v[32:33], v[48:49] neg_lo:[0,1] neg_hi:[0,1]
	v_pk_add_f32 v[48:49], v[34:35], v[26:27]
	v_pk_add_f32 v[26:27], v[34:35], v[26:27] neg_lo:[0,1] neg_hi:[0,1]
	v_pk_mul_f32 v[34:35], v[26:27], v[66:67] op_sel:[1,0] op_sel_hi:[0,0] neg_lo:[1,1] neg_hi:[0,1]
	v_pk_fma_f32 v[26:27], v[26:27], v[66:67], v[34:35] op_sel_hi:[1,0,1]
	v_pk_add_f32 v[34:35], v[36:37], v[42:43]
	v_pk_add_f32 v[36:37], v[36:37], v[42:43] neg_lo:[0,1] neg_hi:[0,1]
	v_pk_mul_f32 v[46:47], v[32:33], v[68:69] op_sel:[1,0] op_sel_hi:[0,0] neg_lo:[1,1] neg_hi:[0,1]
	v_xor_b32_e32 v43, 0x80000000, v36
	v_mov_b32_e32 v42, v37
	v_pk_add_f32 v[36:37], v[38:39], v[44:45]
	v_pk_add_f32 v[38:39], v[38:39], v[44:45] neg_lo:[0,1] neg_hi:[0,1]
	v_pk_fma_f32 v[46:47], v[32:33], v[64:65], v[46:47] op_sel_hi:[1,0,1] neg_lo:[0,1,0] neg_hi:[0,1,0]
	v_pk_add_f32 v[32:33], v[70:71], v[40:41]
	v_pk_mul_f32 v[44:45], v[38:39], v[66:67] op_sel:[1,0] op_sel_hi:[0,0] neg_lo:[1,1] neg_hi:[0,1]
	v_pk_add_f32 v[40:41], v[70:71], v[40:41] neg_lo:[0,1] neg_hi:[0,1]
	v_pk_fma_f32 v[38:39], v[38:39], v[66:67], v[44:45] op_sel_hi:[1,0,1] neg_lo:[0,1,0] neg_hi:[0,1,0]
	v_pk_add_f32 v[44:45], v[32:33], v[34:35]
	v_pk_add_f32 v[32:33], v[32:33], v[34:35] neg_lo:[0,1] neg_hi:[0,1]
	v_pk_add_f32 v[34:35], v[48:49], v[36:37]
	v_pk_add_f32 v[36:37], v[48:49], v[36:37] neg_lo:[0,1] neg_hi:[0,1]
	v_pk_add_f32 v[64:65], v[44:45], v[34:35]
	v_xor_b32_e32 v49, 0x80000000, v36
	v_mov_b32_e32 v48, v37
	v_pk_add_f32 v[36:37], v[44:45], v[34:35] neg_lo:[0,1] neg_hi:[0,1]
	v_pk_add_f32 v[68:69], v[32:33], v[48:49]
	v_pk_add_f32 v[44:45], v[32:33], v[48:49] neg_lo:[0,1] neg_hi:[0,1]
	v_pk_add_f32 v[32:33], v[40:41], v[42:43]
	v_pk_add_f32 v[34:35], v[40:41], v[42:43] neg_lo:[0,1] neg_hi:[0,1]
	v_pk_add_f32 v[40:41], v[26:27], v[38:39]
	v_pk_add_f32 v[26:27], v[26:27], v[38:39] neg_lo:[0,1] neg_hi:[0,1]
	v_pk_add_f32 v[42:43], v[32:33], v[40:41] neg_lo:[0,1] neg_hi:[0,1]
	v_xor_b32_e32 v39, 0x80000000, v26
	v_mov_b32_e32 v38, v27
	v_pk_add_f32 v[26:27], v[32:33], v[40:41]
	v_pk_add_f32 v[40:41], v[20:21], v[28:29]
	v_pk_add_f32 v[20:21], v[20:21], v[28:29] neg_lo:[0,1] neg_hi:[0,1]
	v_pk_add_f32 v[32:33], v[34:35], v[38:39]
	v_pk_mul_f32 v[28:29], v[66:67], v[20:21] op_sel:[0,1] op_sel_hi:[0,0] neg_lo:[1,1] neg_hi:[1,0]
	v_pk_fma_f32 v[20:21], v[66:67], v[20:21], v[28:29] op_sel_hi:[0,1,1]
	v_pk_add_f32 v[28:29], v[22:23], v[30:31]
	v_pk_add_f32 v[22:23], v[22:23], v[30:31] neg_lo:[0,1] neg_hi:[0,1]
	v_pk_add_f32 v[38:39], v[34:35], v[38:39] neg_lo:[0,1] neg_hi:[0,1]
	v_xor_b32_e32 v31, 0x80000000, v22
	v_mov_b32_e32 v30, v23
	v_pk_add_f32 v[22:23], v[24:25], v[46:47]
	v_pk_add_f32 v[24:25], v[24:25], v[46:47] neg_lo:[0,1] neg_hi:[0,1]
	v_pk_add_f32 v[34:35], v[18:19], v[72:73]
	v_pk_mul_f32 v[46:47], v[66:67], v[24:25] op_sel:[0,1] op_sel_hi:[0,0] neg_lo:[1,1] neg_hi:[1,0]
	v_pk_fma_f32 v[24:25], v[66:67], v[24:25], v[46:47] op_sel_hi:[0,1,1] neg_lo:[1,0,0] neg_hi:[1,0,0]
	v_pk_add_f32 v[46:47], v[34:35], v[28:29]
	v_pk_add_f32 v[28:29], v[34:35], v[28:29] neg_lo:[0,1] neg_hi:[0,1]
	v_pk_add_f32 v[34:35], v[40:41], v[22:23]
	v_pk_add_f32 v[22:23], v[40:41], v[22:23] neg_lo:[0,1] neg_hi:[0,1]
	v_pk_add_f32 v[18:19], v[18:19], v[72:73] neg_lo:[0,1] neg_hi:[0,1]
	v_pk_add_f32 v[66:67], v[28:29], v[22:23] op_sel:[0,1] op_sel_hi:[1,0] neg_hi:[0,1]
	v_pk_add_f32 v[48:49], v[28:29], v[22:23] op_sel:[0,1] op_sel_hi:[1,0] neg_lo:[0,1]
	v_pk_add_f32 v[28:29], v[18:19], v[30:31]
	v_pk_add_f32 v[18:19], v[18:19], v[30:31] neg_lo:[0,1] neg_hi:[0,1]
	v_pk_add_f32 v[30:31], v[20:21], v[24:25]
	v_pk_add_f32 v[20:21], v[20:21], v[24:25] neg_lo:[0,1] neg_hi:[0,1]
	v_pk_add_f32 v[22:23], v[46:47], v[34:35]
	v_xor_b32_e32 v25, 0x80000000, v20
	v_add_u32_e32 v20, 0x2000, v16
	v_mov_b32_e32 v24, v21
	v_ashrrev_i32_e32 v21, 31, v20
	v_lshl_add_u64 v[20:21], v[20:21], 3, s[48:49]
	s_waitcnt vmcnt(0)
	v_pk_add_f32 v[40:41], v[46:47], v[34:35] neg_lo:[0,1] neg_hi:[0,1]
	v_pk_add_f32 v[34:35], v[18:19], v[24:25]
	v_pk_add_f32 v[18:19], v[18:19], v[24:25] neg_lo:[0,1] neg_hi:[0,1]
	v_pk_add_f32 v[70:71], v[28:29], v[30:31]
	v_pk_add_f32 v[46:47], v[28:29], v[30:31] neg_lo:[0,1] neg_hi:[0,1]
	s_nop 0
	v_pk_mul_f32 v[24:25], v[64:65], v[196:197] op_sel:[1,1] op_sel_hi:[1,0] neg_lo:[1,0]
	v_pk_fma_f32 v[20:21], v[64:65], v[196:197], v[24:25] op_sel_hi:[0,1,1]
	v_add_u32_e32 v24, 0x2200, v16
	v_ashrrev_i32_e32 v25, 31, v24
	v_lshl_add_u64 v[24:25], v[24:25], 3, s[48:49]
	s_nop 0
	v_pk_mul_f32 v[28:29], v[198:199], v[22:23] op_sel:[1,1] op_sel_hi:[0,1] neg_lo:[0,1]
	v_pk_fma_f32 v[22:23], v[198:199], v[22:23], v[28:29] op_sel_hi:[1,0,1]
	v_add_u32_e32 v24, 0x2400, v16
	v_ashrrev_i32_e32 v25, 31, v24
	v_lshl_add_u64 v[24:25], v[24:25], 3, s[48:49]
	s_nop 0
	v_pk_mul_f32 v[28:29], v[26:27], v[200:201] op_sel:[1,1] op_sel_hi:[1,0] neg_lo:[1,0]
	v_pk_fma_f32 v[24:25], v[26:27], v[200:201], v[28:29] op_sel_hi:[0,1,1]
	v_add_u32_e32 v26, 0x2600, v16
	v_ashrrev_i32_e32 v27, 31, v26
	v_lshl_add_u64 v[26:27], v[26:27], 3, s[48:49]
	s_nop 0
	v_pk_mul_f32 v[28:29], v[202:203], v[70:71] op_sel:[1,1] op_sel_hi:[0,1] neg_lo:[0,1]
	v_pk_fma_f32 v[26:27], v[202:203], v[70:71], v[28:29] op_sel_hi:[1,0,1]
	v_add_u32_e32 v28, 0x2800, v16
	v_ashrrev_i32_e32 v29, 31, v28
	v_lshl_add_u64 v[28:29], v[28:29], 3, s[48:49]
	s_nop 0
	v_pk_mul_f32 v[30:31], v[68:69], v[204:205] op_sel:[1,1] op_sel_hi:[1,0] neg_lo:[1,0]
	v_pk_fma_f32 v[28:29], v[68:69], v[204:205], v[30:31] op_sel_hi:[0,1,1]
	v_add_u32_e32 v30, 0x2a00, v16
	v_ashrrev_i32_e32 v31, 31, v30
	v_lshl_add_u64 v[30:31], v[30:31], 3, s[48:49]
	s_nop 0
	v_pk_mul_f32 v[64:65], v[206:207], v[66:67] op_sel:[1,1] op_sel_hi:[0,1] neg_lo:[0,1]
	v_pk_fma_f32 v[30:31], v[206:207], v[66:67], v[64:65] op_sel_hi:[1,0,1]
	v_add_u32_e32 v64, 0x2c00, v16
	v_ashrrev_i32_e32 v65, 31, v64
	v_lshl_add_u64 v[64:65], v[64:65], 3, s[48:49]
	s_nop 0
	v_pk_mul_f32 v[66:67], v[32:33], v[208:209] op_sel:[1,1] op_sel_hi:[1,0] neg_lo:[1,0]
	v_pk_fma_f32 v[32:33], v[32:33], v[208:209], v[66:67] op_sel_hi:[0,1,1]
	v_add_u32_e32 v64, 0x2e00, v16
	v_ashrrev_i32_e32 v65, 31, v64
	v_lshl_add_u64 v[64:65], v[64:65], 3, s[48:49]
	s_nop 0
	v_pk_mul_f32 v[66:67], v[210:211], v[34:35] op_sel:[1,1] op_sel_hi:[0,1] neg_lo:[0,1]
	v_pk_fma_f32 v[34:35], v[210:211], v[34:35], v[66:67] op_sel_hi:[1,0,1]
	v_add_u32_e32 v64, 0x3000, v16
	v_ashrrev_i32_e32 v65, 31, v64
	v_lshl_add_u64 v[64:65], v[64:65], 3, s[48:49]
	s_nop 0
	v_pk_mul_f32 v[66:67], v[36:37], v[212:213] op_sel:[1,1] op_sel_hi:[1,0] neg_lo:[1,0]
	v_pk_fma_f32 v[36:37], v[36:37], v[212:213], v[66:67] op_sel_hi:[0,1,1]
	v_add_u32_e32 v64, 0x3200, v16
	v_ashrrev_i32_e32 v65, 31, v64
	v_lshl_add_u64 v[64:65], v[64:65], 3, s[48:49]
	v_pk_add_f32 v[68:69], v[20:21], v[36:37]
	v_pk_add_f32 v[20:21], v[20:21], v[36:37] neg_lo:[0,1] neg_hi:[0,1]
	s_nop 0
	v_pk_mul_f32 v[66:67], v[40:41], v[214:215] op_sel:[1,1] op_sel_hi:[1,0] neg_lo:[1,0]
	v_pk_fma_f32 v[40:41], v[40:41], v[214:215], v[66:67] op_sel_hi:[0,1,1]
	v_add_u32_e32 v64, 0x3400, v16
	v_ashrrev_i32_e32 v65, 31, v64
	v_lshl_add_u64 v[64:65], v[64:65], 3, s[48:49]
	v_pk_add_f32 v[36:37], v[22:23], v[40:41]
	v_pk_add_f32 v[22:23], v[22:23], v[40:41] neg_lo:[0,1] neg_hi:[0,1]
	s_nop 0
	v_pk_mul_f32 v[66:67], v[42:43], v[216:217] op_sel:[1,1] op_sel_hi:[1,0] neg_lo:[1,0]
	v_pk_fma_f32 v[42:43], v[42:43], v[216:217], v[66:67] op_sel_hi:[0,1,1]
	v_add_u32_e32 v64, 0x3600, v16
	v_ashrrev_i32_e32 v65, 31, v64
	v_lshl_add_u64 v[64:65], v[64:65], 3, s[48:49]
	s_nop 0
	v_pk_mul_f32 v[66:67], v[46:47], v[218:219] op_sel:[1,1] op_sel_hi:[1,0] neg_lo:[1,0]
	v_pk_fma_f32 v[46:47], v[46:47], v[218:219], v[66:67] op_sel_hi:[0,1,1]
	v_add_u32_e32 v64, 0x3800, v16
	v_ashrrev_i32_e32 v65, 31, v64
	v_lshl_add_u64 v[64:65], v[64:65], 3, s[48:49]
	s_nop 0
	v_pk_mul_f32 v[66:67], v[44:45], v[220:221] op_sel:[1,1] op_sel_hi:[1,0] neg_lo:[1,0]
	v_pk_fma_f32 v[44:45], v[44:45], v[220:221], v[66:67] op_sel_hi:[0,1,1]
	v_add_u32_e32 v64, 0x3a00, v16
	v_ashrrev_i32_e32 v65, 31, v64
	v_lshl_add_u64 v[64:65], v[64:65], 3, s[48:49]
	s_nop 0
	v_pk_mul_f32 v[66:67], v[48:49], v[222:223] op_sel:[1,1] op_sel_hi:[1,0] neg_lo:[1,0]
	v_pk_fma_f32 v[48:49], v[48:49], v[222:223], v[66:67] op_sel_hi:[0,1,1]
	v_add_u32_e32 v64, 0x3c00, v16
	v_ashrrev_i32_e32 v65, 31, v64
	v_lshl_add_u64 v[64:65], v[64:65], 3, s[48:49]
	v_add_u32_e32 v16, 0x3e00, v16
	v_ashrrev_i32_e32 v17, 31, v16
	v_lshl_add_u64 v[16:17], v[16:17], 3, s[48:49]
	s_nop 0
	v_pk_mul_f32 v[66:67], v[38:39], v[224:225] op_sel:[1,1] op_sel_hi:[1,0] neg_lo:[1,0]
	v_pk_fma_f32 v[38:39], v[38:39], v[224:225], v[66:67] op_sel_hi:[0,1,1]
	s_nop 0
	v_pk_mul_f32 v[64:65], v[18:19], v[226:227] op_sel:[1,1] op_sel_hi:[1,0] neg_lo:[1,0]
	v_mov_b32_e32 v66, v170
	v_pk_fma_f32 v[16:17], v[18:19], v[226:227], v[64:65] op_sel_hi:[0,1,1]
	v_mov_b32_e32 v18, v164
	v_mov_b32_e32 v19, v167
	v_mov_b32_e32 v18, v165
	v_mov_b32_e32 v64, v168
	v_mov_b32_e32 v18, v166
	s_nop 0
	v_mov_b32_e32 v19, v169
	s_nop 0
	v_mov_b32_e32 v19, v171
	v_pk_mul_f32 v[40:41], v[22:23], v[66:67] op_sel:[1,0] op_sel_hi:[0,0] neg_lo:[1,0]
	v_mov_b32_e32 v19, v172
	s_nop 0
	v_pk_fma_f32 v[22:23], v[22:23], v[18:19], v[40:41] op_sel_hi:[1,0,1]
	v_pk_add_f32 v[40:41], v[24:25], v[42:43]
	v_pk_add_f32 v[24:25], v[24:25], v[42:43] neg_lo:[0,1] neg_hi:[0,1]
	v_pk_mul_f32 v[42:43], v[24:25], v[64:65] op_sel:[1,0] op_sel_hi:[0,0] neg_lo:[1,0]
	v_pk_fma_f32 v[24:25], v[24:25], v[64:65], v[42:43] op_sel_hi:[1,0,1]
	v_pk_add_f32 v[42:43], v[26:27], v[46:47]
	v_pk_add_f32 v[26:27], v[26:27], v[46:47] neg_lo:[0,1] neg_hi:[0,1]
	v_pk_mul_f32 v[46:47], v[26:27], v[66:67] op_sel_hi:[1,0]
	v_pk_fma_f32 v[26:27], v[26:27], v[18:19], v[46:47] op_sel:[1,0,0] op_sel_hi:[0,0,1] neg_lo:[1,0,0]
	v_pk_add_f32 v[46:47], v[28:29], v[44:45]
	v_pk_add_f32 v[28:29], v[28:29], v[44:45] neg_lo:[0,1] neg_hi:[0,1]
	v_xor_b32_e32 v44, 0x80000000, v29
	v_mov_b32_e32 v45, v28
	v_pk_add_f32 v[28:29], v[30:31], v[48:49]
	v_pk_add_f32 v[30:31], v[30:31], v[48:49] neg_lo:[0,1] neg_hi:[0,1]
	v_pk_mul_f32 v[48:49], v[30:31], v[66:67] op_sel_hi:[1,0] neg_lo:[0,1] neg_hi:[0,1]
	v_pk_fma_f32 v[30:31], v[30:31], v[18:19], v[48:49] op_sel:[1,0,0] op_sel_hi:[0,0,1] neg_lo:[1,0,0]
	v_pk_add_f32 v[48:49], v[32:33], v[38:39]
	v_pk_add_f32 v[32:33], v[32:33], v[38:39] neg_lo:[0,1] neg_hi:[0,1]
	v_pk_mul_f32 v[38:39], v[32:33], v[64:65] op_sel:[1,0] op_sel_hi:[0,0] neg_lo:[1,0]
	v_pk_fma_f32 v[32:33], v[32:33], v[64:65], v[38:39] op_sel_hi:[1,0,1] neg_lo:[0,1,0] neg_hi:[0,1,0]
	v_pk_add_f32 v[38:39], v[34:35], v[16:17]
	v_pk_add_f32 v[16:17], v[34:35], v[16:17] neg_lo:[0,1] neg_hi:[0,1]
	v_pk_mul_f32 v[34:35], v[16:17], v[66:67] op_sel:[1,0] op_sel_hi:[0,0] neg_lo:[1,0]
	v_pk_fma_f32 v[16:17], v[16:17], v[18:19], v[34:35] op_sel_hi:[1,0,1] neg_lo:[0,1,0] neg_hi:[0,1,0]
	v_pk_add_f32 v[18:19], v[68:69], v[46:47]
	v_pk_add_f32 v[34:35], v[68:69], v[46:47] neg_lo:[0,1] neg_hi:[0,1]
	v_pk_add_f32 v[46:47], v[36:37], v[28:29]
	v_pk_add_f32 v[28:29], v[36:37], v[28:29] neg_lo:[0,1] neg_hi:[0,1]
	v_pk_mul_f32 v[36:37], v[28:29], v[64:65] op_sel:[1,0] op_sel_hi:[0,0] neg_lo:[1,0]
	v_pk_fma_f32 v[28:29], v[28:29], v[64:65], v[36:37] op_sel_hi:[1,0,1]
	v_pk_add_f32 v[36:37], v[40:41], v[48:49]
	v_pk_add_f32 v[40:41], v[40:41], v[48:49] neg_lo:[0,1] neg_hi:[0,1]
	v_xor_b32_e32 v48, 0x80000000, v41
	v_mov_b32_e32 v49, v40
	v_pk_add_f32 v[40:41], v[42:43], v[38:39]
	v_pk_add_f32 v[38:39], v[42:43], v[38:39] neg_lo:[0,1] neg_hi:[0,1]
	v_pk_mul_f32 v[42:43], v[64:65], v[38:39] op_sel:[0,1] op_sel_hi:[0,0] neg_lo:[0,1]
	v_pk_fma_f32 v[38:39], v[38:39], v[64:65], v[42:43] op_sel_hi:[1,0,1] neg_lo:[0,1,0] neg_hi:[0,1,0]
	v_pk_add_f32 v[42:43], v[18:19], v[36:37]
	v_pk_add_f32 v[18:19], v[18:19], v[36:37] neg_lo:[0,1] neg_hi:[0,1]
	v_pk_add_f32 v[36:37], v[46:47], v[40:41]
	v_pk_add_f32 v[40:41], v[46:47], v[40:41] neg_lo:[0,1] neg_hi:[0,1]
	v_xor_b32_e32 v46, 0x80000000, v41
	v_mov_b32_e32 v47, v40
	v_pk_add_f32 v[40:41], v[42:43], v[36:37]
	v_pk_add_f32 v[36:37], v[42:43], v[36:37] neg_lo:[0,1] neg_hi:[0,1]
	v_pk_add_f32 v[42:43], v[18:19], v[46:47]
	v_pk_add_f32 v[18:19], v[18:19], v[46:47] neg_lo:[0,1] neg_hi:[0,1]
	v_pk_add_f32 v[46:47], v[34:35], v[48:49]
	v_pk_add_f32 v[34:35], v[34:35], v[48:49] neg_lo:[0,1] neg_hi:[0,1]
	v_pk_add_f32 v[48:49], v[28:29], v[38:39]
	v_pk_add_f32 v[28:29], v[28:29], v[38:39] neg_lo:[0,1] neg_hi:[0,1]
	v_xor_b32_e32 v38, 0x80000000, v29
	v_mov_b32_e32 v39, v28
	v_pk_add_f32 v[28:29], v[46:47], v[48:49]
	v_pk_add_f32 v[46:47], v[46:47], v[48:49] neg_lo:[0,1] neg_hi:[0,1]
	v_pk_add_f32 v[48:49], v[34:35], v[38:39]
	v_pk_add_f32 v[34:35], v[34:35], v[38:39] neg_lo:[0,1] neg_hi:[0,1]
	v_pk_add_f32 v[38:39], v[20:21], v[44:45]
	v_pk_add_f32 v[20:21], v[20:21], v[44:45] neg_lo:[0,1] neg_hi:[0,1]
	v_pk_add_f32 v[44:45], v[22:23], v[30:31]
	v_pk_add_f32 v[22:23], v[22:23], v[30:31] neg_lo:[0,1] neg_hi:[0,1]
	v_pk_mul_f32 v[30:31], v[64:65], v[22:23] op_sel:[0,1] op_sel_hi:[0,0] neg_lo:[0,1]
	v_pk_fma_f32 v[22:23], v[64:65], v[22:23], v[30:31] op_sel_hi:[0,1,1]
	v_pk_add_f32 v[30:31], v[24:25], v[32:33]
	v_pk_add_f32 v[24:25], v[24:25], v[32:33] neg_lo:[0,1] neg_hi:[0,1]
	v_xor_b32_e32 v32, 0x80000000, v25
	v_mov_b32_e32 v33, v24
	v_pk_add_f32 v[24:25], v[26:27], v[16:17]
	v_pk_add_f32 v[16:17], v[26:27], v[16:17] neg_lo:[0,1] neg_hi:[0,1]
	v_pk_mul_f32 v[26:27], v[64:65], v[16:17] op_sel:[0,1] op_sel_hi:[0,0] neg_lo:[0,1]
	v_pk_fma_f32 v[16:17], v[64:65], v[16:17], v[26:27] op_sel_hi:[0,1,1] neg_lo:[1,0,0] neg_hi:[1,0,0]
	v_pk_add_f32 v[26:27], v[38:39], v[30:31]
	v_pk_add_f32 v[30:31], v[38:39], v[30:31] neg_lo:[0,1] neg_hi:[0,1]
	v_pk_add_f32 v[38:39], v[44:45], v[24:25]
	v_pk_add_f32 v[24:25], v[44:45], v[24:25] neg_lo:[0,1] neg_hi:[0,1]
	v_xor_b32_e32 v44, 0x80000000, v25
	v_mov_b32_e32 v45, v24
	v_pk_add_f32 v[24:25], v[26:27], v[38:39]
	v_pk_add_f32 v[26:27], v[26:27], v[38:39] neg_lo:[0,1] neg_hi:[0,1]
	v_pk_add_f32 v[38:39], v[30:31], v[44:45]
	v_pk_add_f32 v[30:31], v[30:31], v[44:45] neg_lo:[0,1] neg_hi:[0,1]
	v_pk_add_f32 v[44:45], v[20:21], v[32:33]
	v_pk_add_f32 v[20:21], v[20:21], v[32:33] neg_lo:[0,1] neg_hi:[0,1]
	v_pk_add_f32 v[32:33], v[22:23], v[16:17]
	v_pk_add_f32 v[16:17], v[22:23], v[16:17] neg_lo:[0,1] neg_hi:[0,1]
	v_xor_b32_e32 v22, 0x80000000, v17
	v_mov_b32_e32 v23, v16
	v_pk_add_f32 v[16:17], v[44:45], v[32:33]
	v_pk_add_f32 v[32:33], v[44:45], v[32:33] neg_lo:[0,1] neg_hi:[0,1]
	v_pk_add_f32 v[44:45], v[20:21], v[22:23]
	v_pk_add_f32 v[20:21], v[20:21], v[22:23] neg_lo:[0,1] neg_hi:[0,1]
	ds_write_b64 v10, v[40:41]
	ds_write_b64 v13, v[24:25]
	ds_write_b64 v15, v[28:29]
	ds_write_b64 v50, v[16:17]
	ds_write_b64 v51, v[42:43]
	ds_write_b64 v52, v[38:39]
	ds_write_b64 v53, v[48:49]
	ds_write_b64 v54, v[44:45]
	ds_write_b64 v55, v[36:37]
	ds_write_b64 v56, v[26:27]
	ds_write_b64 v57, v[46:47]
	ds_write_b64 v58, v[32:33]
	ds_write_b64 v59, v[18:19]
	ds_write_b64 v60, v[30:31]
	ds_write_b64 v61, v[34:35]
	ds_write_b64 v62, v[20:21]
	v_mov_b32_e32 v10, v176
	v_mov_b32_e32 v50, v173
	s_waitcnt lgkmcnt(0)
	s_barrier
	v_add_u32_e32 v13, v50, v10
	v_lshl_add_u32 v13, v13, 3, 0
	ds_read2_b64 v[16:19], v13 offset1:16
	v_xad_u32 v15, v50, 1, v10
	v_lshl_add_u32 v15, v15, 3, 0
	s_waitcnt lgkmcnt(0)
	v_pk_fma_f32 v[16:17], v[16:17], 0, v[16:17] op_sel:[1,0,0] op_sel_hi:[0,0,1] neg_hi:[1,0,0]
	v_pk_fma_f32 v[22:23], v[182:183], s[92:93], v[182:183] op_sel:[1,0,0] op_sel_hi:[0,1,1]
	v_pk_mul_f32 v[24:25], v[22:23], v[18:19] op_sel:[1,1] op_sel_hi:[1,0] neg_hi:[0,1]
	v_pk_fma_f32 v[18:19], v[18:19], v[22:23], v[24:25] op_sel_hi:[1,0,1]
	v_pk_mul_f32 v[24:25], v[182:183], v[22:23] op_sel:[1,1] op_sel_hi:[0,1] neg_lo:[0,1]
	v_pk_fma_f32 v[26:27], v[182:183], v[22:23], v[24:25] op_sel_hi:[1,0,1]
	ds_read2_b64 v[22:25], v15 offset0:32 offset1:48
	s_waitcnt lgkmcnt(0)
	v_pk_mul_f32 v[28:29], v[22:23], v[26:27] op_sel:[1,1] op_sel_hi:[0,1] neg_hi:[1,0]
	v_pk_fma_f32 v[22:23], v[22:23], v[26:27], v[28:29] op_sel_hi:[1,0,1]
	v_pk_mul_f32 v[28:29], v[182:183], v[26:27] op_sel:[1,1] op_sel_hi:[0,1] neg_lo:[0,1]
	v_pk_fma_f32 v[26:27], v[182:183], v[26:27], v[28:29] op_sel_hi:[1,0,1]
	v_pk_mul_f32 v[28:29], v[24:25], v[26:27] op_sel:[1,1] op_sel_hi:[0,1] neg_hi:[1,0]
	v_pk_fma_f32 v[24:25], v[24:25], v[26:27], v[28:29] op_sel_hi:[1,0,1]
	v_pk_mul_f32 v[28:29], v[182:183], v[26:27] op_sel:[1,1] op_sel_hi:[0,1] neg_lo:[0,1]
	v_pk_fma_f32 v[26:27], v[182:183], v[26:27], v[28:29] op_sel_hi:[1,0,1]
	v_xad_u32 v28, v50, 2, v10
	v_lshl_add_u32 v51, v28, 3, 0
	ds_read2_b64 v[28:31], v51 offset0:64 offset1:80
	v_pk_mul_f32 v[32:33], v[182:183], v[26:27] op_sel:[1,1] op_sel_hi:[0,1] neg_lo:[0,1]
	s_waitcnt lgkmcnt(0)
	v_pk_mul_f32 v[34:35], v[28:29], v[26:27] op_sel:[1,1] op_sel_hi:[0,1] neg_hi:[1,0]
	v_pk_fma_f32 v[28:29], v[28:29], v[26:27], v[34:35] op_sel_hi:[1,0,1]
	v_pk_fma_f32 v[34:35], v[182:183], v[26:27], v[32:33] op_sel_hi:[1,0,1]
	v_pk_mul_f32 v[26:27], v[30:31], v[34:35] op_sel:[1,1] op_sel_hi:[0,1] neg_hi:[1,0]
	v_pk_fma_f32 v[26:27], v[30:31], v[34:35], v[26:27] op_sel_hi:[1,0,1]
	v_xad_u32 v30, v50, 3, v10
	v_lshl_add_u32 v54, v30, 3, 0
	ds_read2_b64 v[30:33], v54 offset0:96 offset1:112
	v_pk_mul_f32 v[36:37], v[182:183], v[34:35] op_sel:[1,1] op_sel_hi:[0,1] neg_lo:[0,1]
	v_pk_fma_f32 v[34:35], v[182:183], v[34:35], v[36:37] op_sel_hi:[1,0,1]
	s_waitcnt lgkmcnt(0)
	v_pk_mul_f32 v[36:37], v[30:31], v[34:35] op_sel:[1,1] op_sel_hi:[0,1] neg_hi:[1,0]
	v_pk_fma_f32 v[30:31], v[30:31], v[34:35], v[36:37] op_sel_hi:[1,0,1]
	v_pk_mul_f32 v[36:37], v[182:183], v[34:35] op_sel:[1,1] op_sel_hi:[0,1] neg_lo:[0,1]
	v_pk_fma_f32 v[34:35], v[182:183], v[34:35], v[36:37] op_sel_hi:[1,0,1]
	v_pk_mul_f32 v[36:37], v[32:33], v[34:35] op_sel:[1,1] op_sel_hi:[0,1] neg_hi:[1,0]
	v_pk_fma_f32 v[32:33], v[32:33], v[34:35], v[36:37] op_sel_hi:[1,0,1]
	v_pk_mul_f32 v[36:37], v[182:183], v[34:35] op_sel:[1,1] op_sel_hi:[0,1] neg_lo:[0,1]
	v_pk_fma_f32 v[38:39], v[182:183], v[34:35], v[36:37] op_sel_hi:[1,0,1]
	v_xad_u32 v34, v50, 4, v10
	v_lshl_add_u32 v55, v34, 3, 0
	ds_read2_b64 v[34:37], v55 offset0:128 offset1:144
	v_pk_mul_f32 v[40:41], v[182:183], v[38:39] op_sel:[1,1] op_sel_hi:[0,1] neg_lo:[0,1]
	s_waitcnt lgkmcnt(0)
	v_pk_mul_f32 v[42:43], v[34:35], v[38:39] op_sel:[1,1] op_sel_hi:[0,1] neg_hi:[1,0]
	v_pk_fma_f32 v[34:35], v[34:35], v[38:39], v[42:43] op_sel_hi:[1,0,1]
	v_pk_fma_f32 v[42:43], v[182:183], v[38:39], v[40:41] op_sel_hi:[1,0,1]
	v_pk_mul_f32 v[38:39], v[36:37], v[42:43] op_sel:[1,1] op_sel_hi:[0,1] neg_hi:[1,0]
	v_pk_fma_f32 v[36:37], v[36:37], v[42:43], v[38:39] op_sel_hi:[1,0,1]
	v_xad_u32 v38, v50, 5, v10
	v_lshl_add_u32 v56, v38, 3, 0
	ds_read2_b64 v[38:41], v56 offset0:160 offset1:176
	v_pk_mul_f32 v[44:45], v[182:183], v[42:43] op_sel:[1,1] op_sel_hi:[0,1] neg_lo:[0,1]
	v_pk_fma_f32 v[42:43], v[182:183], v[42:43], v[44:45] op_sel_hi:[1,0,1]
	s_waitcnt lgkmcnt(0)
	v_pk_mul_f32 v[44:45], v[38:39], v[42:43] op_sel:[1,1] op_sel_hi:[0,1] neg_hi:[1,0]
	v_pk_fma_f32 v[38:39], v[38:39], v[42:43], v[44:45] op_sel_hi:[1,0,1]
	v_pk_mul_f32 v[44:45], v[182:183], v[42:43] op_sel:[1,1] op_sel_hi:[0,1] neg_lo:[0,1]
	v_pk_fma_f32 v[42:43], v[182:183], v[42:43], v[44:45] op_sel_hi:[1,0,1]
	v_pk_mul_f32 v[44:45], v[40:41], v[42:43] op_sel:[1,1] op_sel_hi:[0,1] neg_hi:[1,0]
	v_pk_fma_f32 v[40:41], v[40:41], v[42:43], v[44:45] op_sel_hi:[1,0,1]
	v_pk_mul_f32 v[44:45], v[182:183], v[42:43] op_sel:[1,1] op_sel_hi:[0,1] neg_lo:[0,1]
	v_pk_fma_f32 v[42:43], v[182:183], v[42:43], v[44:45] op_sel_hi:[1,0,1]
	v_xad_u32 v44, v50, 6, v10
	v_lshl_add_u32 v57, v44, 3, 0
	ds_read2_b64 v[44:47], v57 offset0:192 offset1:208
	v_pk_mul_f32 v[48:49], v[182:183], v[42:43] op_sel:[1,1] op_sel_hi:[0,1] neg_lo:[0,1]
	s_waitcnt lgkmcnt(0)
	v_pk_mul_f32 v[52:53], v[44:45], v[42:43] op_sel:[1,1] op_sel_hi:[0,1] neg_hi:[1,0]
	v_pk_fma_f32 v[44:45], v[44:45], v[42:43], v[52:53] op_sel_hi:[1,0,1]
	v_pk_fma_f32 v[52:53], v[182:183], v[42:43], v[48:49] op_sel_hi:[1,0,1]
	v_pk_mul_f32 v[42:43], v[46:47], v[52:53] op_sel:[1,1] op_sel_hi:[0,1] neg_hi:[1,0]
	v_pk_fma_f32 v[42:43], v[46:47], v[52:53], v[42:43] op_sel_hi:[1,0,1]
	v_xad_u32 v46, v50, 7, v10
	v_lshl_add_u32 v58, v46, 3, 0
	ds_read2_b64 v[46:49], v58 offset0:224 offset1:240
	v_pk_mul_f32 v[60:61], v[182:183], v[52:53] op_sel:[1,1] op_sel_hi:[0,1] neg_lo:[0,1]
	v_pk_fma_f32 v[52:53], v[182:183], v[52:53], v[60:61] op_sel_hi:[1,0,1]
	s_waitcnt lgkmcnt(0)
	v_pk_mul_f32 v[60:61], v[46:47], v[52:53] op_sel:[1,1] op_sel_hi:[0,1] neg_hi:[1,0]
	v_pk_fma_f32 v[46:47], v[46:47], v[52:53], v[60:61] op_sel_hi:[1,0,1]
	v_pk_mul_f32 v[60:61], v[182:183], v[52:53] op_sel:[1,1] op_sel_hi:[0,1] neg_lo:[0,1]
	v_pk_fma_f32 v[52:53], v[182:183], v[52:53], v[60:61] op_sel_hi:[1,0,1]
	v_pk_mul_f32 v[60:61], v[48:49], v[52:53] op_sel:[1,1] op_sel_hi:[0,1] neg_hi:[1,0]
	v_pk_fma_f32 v[48:49], v[48:49], v[52:53], v[60:61] op_sel_hi:[1,0,1]
	v_pk_mul_f32 v[60:61], v[182:183], v[52:53] op_sel:[1,1] op_sel_hi:[0,1] neg_lo:[0,1]
	v_pk_fma_f32 v[64:65], v[182:183], v[52:53], v[60:61] op_sel_hi:[1,0,1]
	v_xad_u32 v52, v50, 8, v10
	v_lshl_add_u32 v52, v52, 3, 0
	v_add_u32_e32 v59, 0x800, v52
	ds_read2_b64 v[60:63], v59 offset1:16
	v_pk_mul_f32 v[66:67], v[182:183], v[64:65] op_sel:[1,1] op_sel_hi:[0,1] neg_lo:[0,1]
	v_pk_fma_f32 v[66:67], v[182:183], v[64:65], v[66:67] op_sel_hi:[1,0,1]
	s_waitcnt lgkmcnt(0)
	v_pk_mul_f32 v[52:53], v[60:61], v[64:65] op_sel:[1,1] op_sel_hi:[0,1] neg_hi:[1,0]
	v_pk_fma_f32 v[52:53], v[60:61], v[64:65], v[52:53] op_sel_hi:[1,0,1]
	v_pk_mul_f32 v[60:61], v[62:63], v[66:67] op_sel:[1,1] op_sel_hi:[0,1] neg_hi:[1,0]
	v_pk_fma_f32 v[70:71], v[62:63], v[66:67], v[60:61] op_sel_hi:[1,0,1]
	v_xad_u32 v60, v50, 9, v10
	v_lshl_add_u32 v60, v60, 3, 0
	v_add_u32_e32 v60, 0x800, v60
	ds_read2_b64 v[62:65], v60 offset0:32 offset1:48
	v_pk_mul_f32 v[68:69], v[182:183], v[66:67] op_sel:[1,1] op_sel_hi:[0,1] neg_lo:[0,1]
	v_pk_fma_f32 v[66:67], v[182:183], v[66:67], v[68:69] op_sel_hi:[1,0,1]
	s_waitcnt lgkmcnt(0)
	v_pk_mul_f32 v[68:69], v[62:63], v[66:67] op_sel:[1,1] op_sel_hi:[0,1] neg_hi:[1,0]
	v_pk_fma_f32 v[72:73], v[62:63], v[66:67], v[68:69] op_sel_hi:[1,0,1]
	v_pk_mul_f32 v[62:63], v[182:183], v[66:67] op_sel:[1,1] op_sel_hi:[0,1] neg_lo:[0,1]
	v_pk_fma_f32 v[62:63], v[182:183], v[66:67], v[62:63] op_sel_hi:[1,0,1]
	v_pk_mul_f32 v[66:67], v[64:65], v[62:63] op_sel:[1,1] op_sel_hi:[0,1] neg_hi:[1,0]
	v_pk_fma_f32 v[74:75], v[64:65], v[62:63], v[66:67] op_sel_hi:[1,0,1]
	v_pk_mul_f32 v[64:65], v[182:183], v[62:63] op_sel:[1,1] op_sel_hi:[0,1] neg_lo:[0,1]
	v_pk_fma_f32 v[66:67], v[182:183], v[62:63], v[64:65] op_sel_hi:[1,0,1]
	v_xad_u32 v61, v50, 10, v10
	v_lshl_add_u32 v61, v61, 3, 0
	v_add_u32_e32 v61, 0x800, v61
	ds_read2_b64 v[62:65], v61 offset0:64 offset1:80
	v_pk_mul_f32 v[68:69], v[182:183], v[66:67] op_sel:[1,1] op_sel_hi:[0,1] neg_lo:[0,1]
	v_pk_fma_f32 v[68:69], v[182:183], v[66:67], v[68:69] op_sel_hi:[1,0,1]
	s_waitcnt lgkmcnt(0)
	v_pk_mul_f32 v[76:77], v[62:63], v[66:67] op_sel:[1,1] op_sel_hi:[0,1] neg_hi:[1,0]
	v_pk_fma_f32 v[76:77], v[62:63], v[66:67], v[76:77] op_sel_hi:[1,0,1]
	v_pk_mul_f32 v[62:63], v[64:65], v[68:69] op_sel:[1,1] op_sel_hi:[0,1] neg_hi:[1,0]
	v_pk_fma_f32 v[78:79], v[64:65], v[68:69], v[62:63] op_sel_hi:[1,0,1]
	v_xad_u32 v62, v50, 11, v10
	v_lshl_add_u32 v62, v62, 3, 0
	v_add_u32_e32 v62, 0x800, v62
	ds_read2_b64 v[64:67], v62 offset0:96 offset1:112
	v_pk_mul_f32 v[80:81], v[182:183], v[68:69] op_sel:[1,1] op_sel_hi:[0,1] neg_lo:[0,1]
	v_pk_fma_f32 v[68:69], v[182:183], v[68:69], v[80:81] op_sel_hi:[1,0,1]
	s_waitcnt lgkmcnt(0)
	v_pk_mul_f32 v[80:81], v[64:65], v[68:69] op_sel:[1,1] op_sel_hi:[0,1] neg_hi:[1,0]
	v_pk_fma_f32 v[80:81], v[64:65], v[68:69], v[80:81] op_sel_hi:[1,0,1]
	v_pk_mul_f32 v[64:65], v[182:183], v[68:69] op_sel:[1,1] op_sel_hi:[0,1] neg_lo:[0,1]
	v_pk_fma_f32 v[64:65], v[182:183], v[68:69], v[64:65] op_sel_hi:[1,0,1]
	v_pk_mul_f32 v[68:69], v[66:67], v[64:65] op_sel:[1,1] op_sel_hi:[0,1] neg_hi:[1,0]
	v_pk_fma_f32 v[82:83], v[66:67], v[64:65], v[68:69] op_sel_hi:[1,0,1]
	v_pk_mul_f32 v[66:67], v[182:183], v[64:65] op_sel:[1,1] op_sel_hi:[0,1] neg_lo:[0,1]
	v_pk_fma_f32 v[68:69], v[182:183], v[64:65], v[66:67] op_sel_hi:[1,0,1]
	v_xad_u32 v63, v50, 12, v10
	v_lshl_add_u32 v63, v63, 3, 0
	v_add_u32_e32 v63, 0x800, v63
	ds_read2_b64 v[64:67], v63 offset0:128 offset1:144
	v_pk_mul_f32 v[84:85], v[182:183], v[68:69] op_sel:[1,1] op_sel_hi:[0,1] neg_lo:[0,1]
	v_pk_fma_f32 v[84:85], v[182:183], v[68:69], v[84:85] op_sel_hi:[1,0,1]
	s_waitcnt lgkmcnt(0)
	v_pk_mul_f32 v[86:87], v[64:65], v[68:69] op_sel:[1,1] op_sel_hi:[0,1] neg_hi:[1,0]
	v_pk_fma_f32 v[86:87], v[64:65], v[68:69], v[86:87] op_sel_hi:[1,0,1]
	v_pk_mul_f32 v[64:65], v[66:67], v[84:85] op_sel:[1,1] op_sel_hi:[0,1] neg_hi:[1,0]
	v_pk_fma_f32 v[88:89], v[66:67], v[84:85], v[64:65] op_sel_hi:[1,0,1]
	v_xad_u32 v64, v50, 13, v10
	v_lshl_add_u32 v64, v64, 3, 0
	v_add_u32_e32 v64, 0x800, v64
	ds_read2_b64 v[66:69], v64 offset0:160 offset1:176
	v_pk_mul_f32 v[90:91], v[182:183], v[84:85] op_sel:[1,1] op_sel_hi:[0,1] neg_lo:[0,1]
	v_pk_fma_f32 v[84:85], v[182:183], v[84:85], v[90:91] op_sel_hi:[1,0,1]
	s_waitcnt lgkmcnt(0)
	v_pk_mul_f32 v[90:91], v[66:67], v[84:85] op_sel:[1,1] op_sel_hi:[0,1] neg_hi:[1,0]
	v_pk_fma_f32 v[90:91], v[66:67], v[84:85], v[90:91] op_sel_hi:[1,0,1]
	v_pk_mul_f32 v[66:67], v[182:183], v[84:85] op_sel:[1,1] op_sel_hi:[0,1] neg_lo:[0,1]
	v_pk_fma_f32 v[66:67], v[182:183], v[84:85], v[66:67] op_sel_hi:[1,0,1]
	v_pk_mul_f32 v[84:85], v[68:69], v[66:67] op_sel:[1,1] op_sel_hi:[0,1] neg_hi:[1,0]
	v_pk_fma_f32 v[84:85], v[68:69], v[66:67], v[84:85] op_sel_hi:[1,0,1]
	v_pk_mul_f32 v[68:69], v[182:183], v[66:67] op_sel:[1,1] op_sel_hi:[0,1] neg_lo:[0,1]
	v_pk_fma_f32 v[92:93], v[182:183], v[66:67], v[68:69] op_sel_hi:[1,0,1]
	v_xad_u32 v65, v50, 14, v10
	v_lshl_add_u32 v65, v65, 3, 0
	v_add_u32_e32 v65, 0x800, v65
	ds_read2_b64 v[66:69], v65 offset0:192 offset1:208
	v_pk_mul_f32 v[94:95], v[182:183], v[92:93] op_sel:[1,1] op_sel_hi:[0,1] neg_lo:[0,1]
	v_xad_u32 v10, v50, 15, v10
	s_waitcnt lgkmcnt(0)
	v_pk_mul_f32 v[96:97], v[66:67], v[92:93] op_sel:[1,1] op_sel_hi:[0,1] neg_hi:[1,0]
	v_lshl_add_u32 v10, v10, 3, 0
	v_pk_fma_f32 v[96:97], v[66:67], v[92:93], v[96:97] op_sel_hi:[1,0,1]
	v_pk_fma_f32 v[92:93], v[182:183], v[92:93], v[94:95] op_sel_hi:[1,0,1]
	v_pk_mul_f32 v[66:67], v[68:69], v[92:93] op_sel:[1,1] op_sel_hi:[0,1] neg_hi:[1,0]
	v_add_u32_e32 v101, 0x800, v10
	v_pk_fma_f32 v[94:95], v[68:69], v[92:93], v[66:67] op_sel_hi:[1,0,1]
	ds_read2_b64 v[66:69], v101 offset0:224 offset1:240
	v_pk_mul_f32 v[98:99], v[182:183], v[92:93] op_sel:[1,1] op_sel_hi:[0,1] neg_lo:[0,1]
	v_pk_fma_f32 v[92:93], v[182:183], v[92:93], v[98:99] op_sel_hi:[1,0,1]
	s_waitcnt lgkmcnt(0)
	v_pk_mul_f32 v[98:99], v[66:67], v[92:93] op_sel:[1,1] op_sel_hi:[0,1] neg_hi:[1,0]
	v_pk_fma_f32 v[66:67], v[66:67], v[92:93], v[98:99] op_sel_hi:[1,0,1]
	v_pk_mul_f32 v[98:99], v[182:183], v[92:93] op_sel:[1,1] op_sel_hi:[0,1] neg_lo:[0,1]
	v_pk_fma_f32 v[20:21], v[182:183], v[92:93], v[98:99] op_sel_hi:[1,0,1]
	v_pk_mul_f32 v[92:93], v[68:69], v[20:21] op_sel:[1,1] op_sel_hi:[0,1] neg_hi:[1,0]
	v_pk_fma_f32 v[68:69], v[68:69], v[20:21], v[92:93] op_sel_hi:[1,0,1]
	v_mov_b32_e32 v10, v164
	v_pk_add_f32 v[104:105], v[16:17], v[52:53]
	v_pk_add_f32 v[16:17], v[16:17], v[52:53] neg_lo:[0,1] neg_hi:[0,1]
	v_pk_add_f32 v[52:53], v[18:19], v[70:71]
	v_pk_add_f32 v[18:19], v[18:19], v[70:71] neg_lo:[0,1] neg_hi:[0,1]
	v_mov_b32_e32 v92, v165
	v_mov_b32_e32 v20, v166
	v_mov_b32_e32 v98, v167
	v_mov_b32_e32 v10, v168
	v_mov_b32_e32 v100, v169
	v_mov_b32_e32 v50, v170
	v_mov_b32_e32 v102, v171
	v_mov_b32_e32 v21, v172
	v_pk_mul_f32 v[70:71], v[102:103], v[18:19] op_sel:[0,1] op_sel_hi:[0,0] neg_lo:[0,1]
	v_pk_fma_f32 v[18:19], v[92:93], v[18:19], v[70:71] op_sel_hi:[0,1,1]
	v_pk_add_f32 v[70:71], v[22:23], v[72:73]
	v_pk_add_f32 v[22:23], v[22:23], v[72:73] neg_lo:[0,1] neg_hi:[0,1]
	v_pk_mul_f32 v[72:73], v[50:51], v[22:23] op_sel:[0,1] op_sel_hi:[0,0] neg_lo:[0,1]
	v_pk_fma_f32 v[22:23], v[20:21], v[22:23], v[72:73] op_sel_hi:[0,1,1]
	v_pk_add_f32 v[72:73], v[24:25], v[74:75]
	v_pk_add_f32 v[24:25], v[24:25], v[74:75] neg_lo:[0,1] neg_hi:[0,1]
	v_pk_mul_f32 v[74:75], v[100:101], v[24:25] op_sel:[0,1] op_sel_hi:[0,0] neg_lo:[0,1]
	v_pk_fma_f32 v[24:25], v[98:99], v[24:25], v[74:75] op_sel_hi:[0,1,1]
	v_pk_add_f32 v[74:75], v[28:29], v[76:77]
	v_pk_add_f32 v[28:29], v[28:29], v[76:77] neg_lo:[0,1] neg_hi:[0,1]
	v_pk_mul_f32 v[76:77], v[10:11], v[28:29] op_sel:[0,1] op_sel_hi:[0,0] neg_lo:[0,1]
	v_pk_fma_f32 v[28:29], v[10:11], v[28:29], v[76:77] op_sel_hi:[0,1,1]
	v_pk_add_f32 v[76:77], v[26:27], v[78:79]
	v_pk_add_f32 v[26:27], v[26:27], v[78:79] neg_lo:[0,1] neg_hi:[0,1]
	v_pk_mul_f32 v[78:79], v[98:99], v[26:27] op_sel:[0,1] op_sel_hi:[0,0] neg_lo:[0,1]
	v_pk_fma_f32 v[26:27], v[100:101], v[26:27], v[78:79] op_sel_hi:[0,1,1]
	v_pk_add_f32 v[78:79], v[30:31], v[80:81]
	v_pk_add_f32 v[30:31], v[30:31], v[80:81] neg_lo:[0,1] neg_hi:[0,1]
	v_pk_mul_f32 v[80:81], v[20:21], v[30:31] op_sel:[0,1] op_sel_hi:[0,0] neg_lo:[0,1]
	v_pk_fma_f32 v[30:31], v[50:51], v[30:31], v[80:81] op_sel_hi:[0,1,1]
	v_pk_add_f32 v[80:81], v[32:33], v[82:83]
	v_pk_add_f32 v[32:33], v[32:33], v[82:83] neg_lo:[0,1] neg_hi:[0,1]
	v_pk_mul_f32 v[82:83], v[92:93], v[32:33] op_sel:[0,1] op_sel_hi:[0,0] neg_lo:[0,1]
	v_pk_fma_f32 v[32:33], v[102:103], v[32:33], v[82:83] op_sel_hi:[0,1,1]
	v_pk_add_f32 v[82:83], v[34:35], v[86:87]
	v_pk_add_f32 v[34:35], v[34:35], v[86:87] neg_lo:[0,1] neg_hi:[0,1]
	v_xor_b32_e32 v86, 0x80000000, v35
	v_mov_b32_e32 v87, v34
	v_pk_add_f32 v[34:35], v[36:37], v[88:89]
	v_pk_add_f32 v[36:37], v[36:37], v[88:89] neg_lo:[0,1] neg_hi:[0,1]
	v_pk_mul_f32 v[88:89], v[92:93], v[36:37] op_sel:[0,1] op_sel_hi:[0,0] neg_lo:[0,1]
	v_pk_fma_f32 v[36:37], v[102:103], v[36:37], v[88:89] op_sel_hi:[0,1,1] neg_lo:[1,0,0] neg_hi:[1,0,0]
	v_pk_add_f32 v[88:89], v[38:39], v[90:91]
	v_pk_add_f32 v[38:39], v[38:39], v[90:91] neg_lo:[0,1] neg_hi:[0,1]
	v_pk_mul_f32 v[90:91], v[20:21], v[38:39] op_sel:[0,1] op_sel_hi:[0,0] neg_lo:[0,1]
	v_pk_fma_f32 v[38:39], v[50:51], v[38:39], v[90:91] op_sel_hi:[0,1,1] neg_lo:[1,0,0] neg_hi:[1,0,0]
	v_pk_add_f32 v[90:91], v[40:41], v[84:85]
	v_pk_add_f32 v[40:41], v[40:41], v[84:85] neg_lo:[0,1] neg_hi:[0,1]
	v_pk_mul_f32 v[84:85], v[98:99], v[40:41] op_sel:[0,1] op_sel_hi:[0,0] neg_lo:[0,1]
	v_pk_fma_f32 v[40:41], v[100:101], v[40:41], v[84:85] op_sel_hi:[0,1,1] neg_lo:[1,0,0] neg_hi:[1,0,0]
	v_pk_add_f32 v[84:85], v[44:45], v[96:97]
	v_pk_add_f32 v[44:45], v[44:45], v[96:97] neg_lo:[0,1] neg_hi:[0,1]
	v_pk_mul_f32 v[96:97], v[10:11], v[44:45] op_sel:[0,1] op_sel_hi:[0,0] neg_lo:[0,1]
	v_pk_fma_f32 v[44:45], v[10:11], v[44:45], v[96:97] op_sel_hi:[0,1,1] neg_lo:[1,0,0] neg_hi:[1,0,0]
	v_pk_add_f32 v[96:97], v[42:43], v[94:95]
	v_pk_add_f32 v[42:43], v[42:43], v[94:95] neg_lo:[0,1] neg_hi:[0,1]
	v_pk_mul_f32 v[94:95], v[100:101], v[42:43] op_sel:[0,1] op_sel_hi:[0,0] neg_lo:[0,1]
	v_pk_fma_f32 v[42:43], v[98:99], v[42:43], v[94:95] op_sel_hi:[0,1,1] neg_lo:[1,0,0] neg_hi:[1,0,0]
	v_pk_add_f32 v[94:95], v[46:47], v[66:67]
	v_pk_add_f32 v[46:47], v[46:47], v[66:67] neg_lo:[0,1] neg_hi:[0,1]
	v_pk_mul_f32 v[66:67], v[50:51], v[46:47] op_sel:[0,1] op_sel_hi:[0,0] neg_lo:[0,1]
	v_pk_fma_f32 v[46:47], v[20:21], v[46:47], v[66:67] op_sel_hi:[0,1,1] neg_lo:[1,0,0] neg_hi:[1,0,0]
	v_pk_add_f32 v[66:67], v[48:49], v[68:69]
	v_pk_add_f32 v[48:49], v[48:49], v[68:69] neg_lo:[0,1] neg_hi:[0,1]
	v_pk_mul_f32 v[68:69], v[102:103], v[48:49] op_sel:[0,1] op_sel_hi:[0,0] neg_lo:[0,1]
	v_pk_fma_f32 v[48:49], v[92:93], v[48:49], v[68:69] op_sel_hi:[0,1,1] neg_lo:[1,0,0] neg_hi:[1,0,0]
	v_pk_add_f32 v[92:93], v[52:53], v[34:35]
	v_pk_add_f32 v[34:35], v[52:53], v[34:35] neg_lo:[0,1] neg_hi:[0,1]
	v_pk_add_f32 v[68:69], v[104:105], v[82:83]
	v_pk_mul_f32 v[52:53], v[50:51], v[34:35] op_sel:[0,1] op_sel_hi:[0,0] neg_lo:[0,1]
	v_pk_fma_f32 v[34:35], v[20:21], v[34:35], v[52:53] op_sel_hi:[0,1,1]
	v_pk_add_f32 v[52:53], v[70:71], v[88:89]
	v_pk_add_f32 v[70:71], v[70:71], v[88:89] neg_lo:[0,1] neg_hi:[0,1]
	v_pk_add_f32 v[82:83], v[104:105], v[82:83] neg_lo:[0,1] neg_hi:[0,1]
	v_pk_mul_f32 v[88:89], v[10:11], v[70:71] op_sel:[0,1] op_sel_hi:[0,0] neg_lo:[0,1]
	v_pk_fma_f32 v[70:71], v[10:11], v[70:71], v[88:89] op_sel_hi:[0,1,1]
	v_pk_add_f32 v[88:89], v[72:73], v[90:91]
	v_pk_add_f32 v[72:73], v[72:73], v[90:91] neg_lo:[0,1] neg_hi:[0,1]
	v_pk_mul_f32 v[90:91], v[20:21], v[72:73] op_sel:[0,1] op_sel_hi:[0,0] neg_lo:[0,1]
	v_pk_fma_f32 v[72:73], v[50:51], v[72:73], v[90:91] op_sel_hi:[0,1,1]
	v_pk_add_f32 v[90:91], v[74:75], v[84:85]
	v_pk_add_f32 v[74:75], v[74:75], v[84:85] neg_lo:[0,1] neg_hi:[0,1]
	v_xor_b32_e32 v84, 0x80000000, v75
	v_mov_b32_e32 v85, v74
	v_pk_add_f32 v[74:75], v[76:77], v[96:97]
	v_pk_add_f32 v[76:77], v[76:77], v[96:97] neg_lo:[0,1] neg_hi:[0,1]
	v_pk_mul_f32 v[96:97], v[20:21], v[76:77] op_sel:[0,1] op_sel_hi:[0,0] neg_lo:[0,1]
	v_pk_fma_f32 v[76:77], v[50:51], v[76:77], v[96:97] op_sel_hi:[0,1,1] neg_lo:[1,0,0] neg_hi:[1,0,0]
	v_pk_add_f32 v[96:97], v[78:79], v[94:95]
	v_pk_add_f32 v[78:79], v[78:79], v[94:95] neg_lo:[0,1] neg_hi:[0,1]
	v_pk_mul_f32 v[94:95], v[10:11], v[78:79] op_sel:[0,1] op_sel_hi:[0,0] neg_lo:[0,1]
	v_pk_fma_f32 v[78:79], v[10:11], v[78:79], v[94:95] op_sel_hi:[0,1,1] neg_lo:[1,0,0] neg_hi:[1,0,0]
	v_pk_add_f32 v[94:95], v[80:81], v[66:67]
	v_pk_add_f32 v[66:67], v[80:81], v[66:67] neg_lo:[0,1] neg_hi:[0,1]
	v_pk_mul_f32 v[80:81], v[50:51], v[66:67] op_sel:[0,1] op_sel_hi:[0,0] neg_lo:[0,1]
	v_pk_fma_f32 v[66:67], v[20:21], v[66:67], v[80:81] op_sel_hi:[0,1,1] neg_lo:[1,0,0] neg_hi:[1,0,0]
	v_pk_add_f32 v[80:81], v[68:69], v[90:91]
	v_pk_add_f32 v[68:69], v[68:69], v[90:91] neg_lo:[0,1] neg_hi:[0,1]
	v_pk_add_f32 v[90:91], v[92:93], v[74:75]
	v_pk_add_f32 v[74:75], v[92:93], v[74:75] neg_lo:[0,1] neg_hi:[0,1]
	v_pk_mul_f32 v[92:93], v[10:11], v[74:75] op_sel:[0,1] op_sel_hi:[0,0] neg_lo:[0,1]
	v_pk_fma_f32 v[74:75], v[10:11], v[74:75], v[92:93] op_sel_hi:[0,1,1]
	v_pk_add_f32 v[92:93], v[52:53], v[96:97]
	v_pk_add_f32 v[52:53], v[52:53], v[96:97] neg_lo:[0,1] neg_hi:[0,1]
	v_xor_b32_e32 v96, 0x80000000, v53
	v_mov_b32_e32 v97, v52
	v_pk_add_f32 v[52:53], v[88:89], v[94:95]
	v_pk_add_f32 v[88:89], v[88:89], v[94:95] neg_lo:[0,1] neg_hi:[0,1]
	v_pk_mul_f32 v[94:95], v[10:11], v[88:89] op_sel:[0,1] op_sel_hi:[0,0] neg_lo:[0,1]
	v_pk_fma_f32 v[88:89], v[10:11], v[88:89], v[94:95] op_sel_hi:[0,1,1] neg_lo:[1,0,0] neg_hi:[1,0,0]
	v_pk_add_f32 v[94:95], v[80:81], v[92:93]
	v_pk_add_f32 v[80:81], v[80:81], v[92:93] neg_lo:[0,1] neg_hi:[0,1]
	v_pk_add_f32 v[92:93], v[90:91], v[52:53]
	v_pk_add_f32 v[52:53], v[90:91], v[52:53] neg_lo:[0,1] neg_hi:[0,1]
	v_xor_b32_e32 v90, 0x80000000, v53
	v_mov_b32_e32 v91, v52
	v_pk_add_f32 v[52:53], v[94:95], v[92:93]
	v_pk_add_f32 v[92:93], v[94:95], v[92:93] neg_lo:[0,1] neg_hi:[0,1]
	v_pk_add_f32 v[94:95], v[80:81], v[90:91]
	v_pk_add_f32 v[80:81], v[80:81], v[90:91] neg_lo:[0,1] neg_hi:[0,1]
	v_pk_add_f32 v[90:91], v[68:69], v[96:97]
	v_pk_add_f32 v[68:69], v[68:69], v[96:97] neg_lo:[0,1] neg_hi:[0,1]
	v_pk_add_f32 v[96:97], v[74:75], v[88:89]
	v_pk_add_f32 v[74:75], v[74:75], v[88:89] neg_lo:[0,1] neg_hi:[0,1]
	v_xor_b32_e32 v88, 0x80000000, v75
	v_mov_b32_e32 v89, v74
	v_pk_add_f32 v[74:75], v[90:91], v[96:97]
	v_pk_add_f32 v[90:91], v[90:91], v[96:97] neg_lo:[0,1] neg_hi:[0,1]
	v_pk_add_f32 v[96:97], v[68:69], v[88:89]
	v_pk_add_f32 v[68:69], v[68:69], v[88:89] neg_lo:[0,1] neg_hi:[0,1]
	v_pk_add_f32 v[88:89], v[82:83], v[84:85]
	v_pk_add_f32 v[82:83], v[82:83], v[84:85] neg_lo:[0,1] neg_hi:[0,1]
	v_pk_add_f32 v[84:85], v[34:35], v[76:77]
	v_pk_add_f32 v[34:35], v[34:35], v[76:77] neg_lo:[0,1] neg_hi:[0,1]
	v_pk_mul_f32 v[76:77], v[10:11], v[34:35] op_sel:[0,1] op_sel_hi:[0,0] neg_lo:[0,1]
	v_pk_fma_f32 v[34:35], v[10:11], v[34:35], v[76:77] op_sel_hi:[0,1,1]
	v_pk_add_f32 v[76:77], v[70:71], v[78:79]
	v_pk_add_f32 v[70:71], v[70:71], v[78:79] neg_lo:[0,1] neg_hi:[0,1]
	v_xor_b32_e32 v78, 0x80000000, v71
	v_mov_b32_e32 v79, v70
	v_pk_add_f32 v[70:71], v[72:73], v[66:67]
	v_pk_add_f32 v[66:67], v[72:73], v[66:67] neg_lo:[0,1] neg_hi:[0,1]
	v_pk_mul_f32 v[72:73], v[10:11], v[66:67] op_sel:[0,1] op_sel_hi:[0,0] neg_lo:[0,1]
	v_pk_fma_f32 v[66:67], v[10:11], v[66:67], v[72:73] op_sel_hi:[0,1,1] neg_lo:[1,0,0] neg_hi:[1,0,0]
	v_pk_add_f32 v[72:73], v[88:89], v[76:77]
	v_pk_add_f32 v[76:77], v[88:89], v[76:77] neg_lo:[0,1] neg_hi:[0,1]
	v_pk_add_f32 v[88:89], v[84:85], v[70:71]
	v_pk_add_f32 v[70:71], v[84:85], v[70:71] neg_lo:[0,1] neg_hi:[0,1]
	v_xor_b32_e32 v84, 0x80000000, v71
	v_mov_b32_e32 v85, v70
	v_pk_add_f32 v[70:71], v[72:73], v[88:89]
	v_pk_add_f32 v[72:73], v[72:73], v[88:89] neg_lo:[0,1] neg_hi:[0,1]
	v_pk_add_f32 v[88:89], v[76:77], v[84:85]
	v_pk_add_f32 v[76:77], v[76:77], v[84:85] neg_lo:[0,1] neg_hi:[0,1]
	v_pk_add_f32 v[84:85], v[82:83], v[78:79]
	v_pk_add_f32 v[78:79], v[82:83], v[78:79] neg_lo:[0,1] neg_hi:[0,1]
	v_pk_add_f32 v[82:83], v[34:35], v[66:67]
	v_pk_add_f32 v[34:35], v[34:35], v[66:67] neg_lo:[0,1] neg_hi:[0,1]
	v_xor_b32_e32 v66, 0x80000000, v35
	v_mov_b32_e32 v67, v34
	v_pk_add_f32 v[34:35], v[84:85], v[82:83]
	v_pk_add_f32 v[82:83], v[84:85], v[82:83] neg_lo:[0,1] neg_hi:[0,1]
	v_pk_add_f32 v[84:85], v[78:79], v[66:67]
	v_pk_add_f32 v[66:67], v[78:79], v[66:67] neg_lo:[0,1] neg_hi:[0,1]
	v_pk_add_f32 v[78:79], v[16:17], v[86:87]
	v_pk_add_f32 v[16:17], v[16:17], v[86:87] neg_lo:[0,1] neg_hi:[0,1]
	v_pk_add_f32 v[86:87], v[18:19], v[36:37]
	v_pk_add_f32 v[18:19], v[18:19], v[36:37] neg_lo:[0,1] neg_hi:[0,1]
	v_pk_mul_f32 v[36:37], v[50:51], v[18:19] op_sel:[0,1] op_sel_hi:[0,0] neg_lo:[0,1]
	v_pk_fma_f32 v[18:19], v[20:21], v[18:19], v[36:37] op_sel_hi:[0,1,1]
	v_pk_add_f32 v[36:37], v[22:23], v[38:39]
	v_pk_add_f32 v[22:23], v[22:23], v[38:39] neg_lo:[0,1] neg_hi:[0,1]
	v_pk_mul_f32 v[38:39], v[10:11], v[22:23] op_sel:[0,1] op_sel_hi:[0,0] neg_lo:[0,1]
	v_pk_fma_f32 v[22:23], v[10:11], v[22:23], v[38:39] op_sel_hi:[0,1,1]
	v_pk_add_f32 v[38:39], v[24:25], v[40:41]
	v_pk_add_f32 v[24:25], v[24:25], v[40:41] neg_lo:[0,1] neg_hi:[0,1]
	v_pk_mul_f32 v[40:41], v[20:21], v[24:25] op_sel:[0,1] op_sel_hi:[0,0] neg_lo:[0,1]
	v_pk_fma_f32 v[24:25], v[50:51], v[24:25], v[40:41] op_sel_hi:[0,1,1]
	v_pk_add_f32 v[40:41], v[28:29], v[44:45]
	v_pk_add_f32 v[28:29], v[28:29], v[44:45] neg_lo:[0,1] neg_hi:[0,1]
	v_xor_b32_e32 v44, 0x80000000, v29
	v_mov_b32_e32 v45, v28
	v_pk_add_f32 v[28:29], v[26:27], v[42:43]
	v_pk_add_f32 v[26:27], v[26:27], v[42:43] neg_lo:[0,1] neg_hi:[0,1]
	v_pk_mul_f32 v[42:43], v[20:21], v[26:27] op_sel:[0,1] op_sel_hi:[0,0] neg_lo:[0,1]
	v_pk_fma_f32 v[26:27], v[50:51], v[26:27], v[42:43] op_sel_hi:[0,1,1] neg_lo:[1,0,0] neg_hi:[1,0,0]
	v_pk_add_f32 v[42:43], v[30:31], v[46:47]
	v_pk_add_f32 v[30:31], v[30:31], v[46:47] neg_lo:[0,1] neg_hi:[0,1]
	v_pk_mul_f32 v[46:47], v[10:11], v[30:31] op_sel:[0,1] op_sel_hi:[0,0] neg_lo:[0,1]
	v_pk_fma_f32 v[30:31], v[10:11], v[30:31], v[46:47] op_sel_hi:[0,1,1] neg_lo:[1,0,0] neg_hi:[1,0,0]
	v_pk_add_f32 v[46:47], v[32:33], v[48:49]
	v_pk_add_f32 v[32:33], v[32:33], v[48:49] neg_lo:[0,1] neg_hi:[0,1]
	v_pk_mul_f32 v[48:49], v[50:51], v[32:33] op_sel:[0,1] op_sel_hi:[0,0] neg_lo:[0,1]
	v_pk_fma_f32 v[20:21], v[20:21], v[32:33], v[48:49] op_sel_hi:[0,1,1] neg_lo:[1,0,0] neg_hi:[1,0,0]
	v_pk_add_f32 v[48:49], v[86:87], v[28:29]
	v_pk_add_f32 v[28:29], v[86:87], v[28:29] neg_lo:[0,1] neg_hi:[0,1]
	v_pk_add_f32 v[32:33], v[78:79], v[40:41]
	v_pk_add_f32 v[40:41], v[78:79], v[40:41] neg_lo:[0,1] neg_hi:[0,1]
	v_pk_mul_f32 v[78:79], v[10:11], v[28:29] op_sel:[0,1] op_sel_hi:[0,0] neg_lo:[0,1]
	v_pk_fma_f32 v[28:29], v[10:11], v[28:29], v[78:79] op_sel_hi:[0,1,1]
	v_pk_add_f32 v[78:79], v[36:37], v[42:43]
	v_pk_add_f32 v[36:37], v[36:37], v[42:43] neg_lo:[0,1] neg_hi:[0,1]
	v_xor_b32_e32 v42, 0x80000000, v37
	v_mov_b32_e32 v43, v36
	v_pk_add_f32 v[36:37], v[38:39], v[46:47]
	v_pk_add_f32 v[38:39], v[38:39], v[46:47] neg_lo:[0,1] neg_hi:[0,1]
	v_pk_mul_f32 v[46:47], v[10:11], v[38:39] op_sel:[0,1] op_sel_hi:[0,0] neg_lo:[0,1]
	v_pk_fma_f32 v[38:39], v[10:11], v[38:39], v[46:47] op_sel_hi:[0,1,1] neg_lo:[1,0,0] neg_hi:[1,0,0]
	v_pk_add_f32 v[46:47], v[32:33], v[78:79]
	v_pk_add_f32 v[32:33], v[32:33], v[78:79] neg_lo:[0,1] neg_hi:[0,1]
	v_pk_add_f32 v[78:79], v[48:49], v[36:37]
	v_pk_add_f32 v[36:37], v[48:49], v[36:37] neg_lo:[0,1] neg_hi:[0,1]
	v_pk_add_f32 v[86:87], v[32:33], v[36:37] op_sel:[0,1] op_sel_hi:[1,0] neg_lo:[0,1]
	v_pk_add_f32 v[32:33], v[32:33], v[36:37] op_sel:[0,1] op_sel_hi:[1,0] neg_hi:[0,1]
	v_pk_add_f32 v[48:49], v[40:41], v[42:43]
	v_pk_add_f32 v[40:41], v[40:41], v[42:43] neg_lo:[0,1] neg_hi:[0,1]
	v_pk_add_f32 v[42:43], v[28:29], v[38:39]
	v_pk_add_f32 v[28:29], v[28:29], v[38:39] neg_lo:[0,1] neg_hi:[0,1]
	v_pk_add_f32 v[36:37], v[46:47], v[78:79] neg_lo:[0,1] neg_hi:[0,1]
	v_xor_b32_e32 v38, 0x80000000, v29
	v_mov_b32_e32 v39, v28
	v_pk_add_f32 v[28:29], v[48:49], v[42:43]
	v_pk_add_f32 v[42:43], v[48:49], v[42:43] neg_lo:[0,1] neg_hi:[0,1]
	v_pk_add_f32 v[48:49], v[40:41], v[38:39]
	v_pk_add_f32 v[38:39], v[40:41], v[38:39] neg_lo:[0,1] neg_hi:[0,1]
	v_pk_add_f32 v[40:41], v[16:17], v[44:45]
	v_pk_add_f32 v[16:17], v[16:17], v[44:45] neg_lo:[0,1] neg_hi:[0,1]
	v_pk_add_f32 v[44:45], v[18:19], v[26:27]
	v_pk_add_f32 v[18:19], v[18:19], v[26:27] neg_lo:[0,1] neg_hi:[0,1]
	v_pk_mul_f32 v[26:27], v[10:11], v[18:19] op_sel:[0,1] op_sel_hi:[0,0] neg_lo:[0,1]
	v_pk_fma_f32 v[18:19], v[10:11], v[18:19], v[26:27] op_sel_hi:[0,1,1]
	v_pk_add_f32 v[26:27], v[22:23], v[30:31]
	v_pk_add_f32 v[22:23], v[22:23], v[30:31] neg_lo:[0,1] neg_hi:[0,1]
	v_xor_b32_e32 v30, 0x80000000, v23
	v_mov_b32_e32 v31, v22
	v_pk_add_f32 v[22:23], v[24:25], v[20:21]
	v_pk_add_f32 v[20:21], v[24:25], v[20:21] neg_lo:[0,1] neg_hi:[0,1]
	v_pk_mul_f32 v[24:25], v[10:11], v[20:21] op_sel:[0,1] op_sel_hi:[0,0] neg_lo:[0,1]
	v_pk_fma_f32 v[20:21], v[10:11], v[20:21], v[24:25] op_sel_hi:[0,1,1] neg_lo:[1,0,0] neg_hi:[1,0,0]
	v_pk_add_f32 v[24:25], v[40:41], v[26:27]
	v_pk_add_f32 v[26:27], v[40:41], v[26:27] neg_lo:[0,1] neg_hi:[0,1]
	v_pk_add_f32 v[40:41], v[44:45], v[22:23]
	v_pk_add_f32 v[22:23], v[44:45], v[22:23] neg_lo:[0,1] neg_hi:[0,1]
	v_xor_b32_e32 v44, 0x80000000, v23
	v_mov_b32_e32 v45, v22
	v_pk_add_f32 v[22:23], v[24:25], v[40:41]
	v_pk_add_f32 v[24:25], v[24:25], v[40:41] neg_lo:[0,1] neg_hi:[0,1]
	v_pk_add_f32 v[40:41], v[26:27], v[44:45]
	v_pk_add_f32 v[26:27], v[26:27], v[44:45] neg_lo:[0,1] neg_hi:[0,1]
	v_pk_add_f32 v[44:45], v[16:17], v[30:31]
	v_pk_add_f32 v[16:17], v[16:17], v[30:31] neg_lo:[0,1] neg_hi:[0,1]
	v_pk_add_f32 v[30:31], v[18:19], v[20:21]
	v_pk_add_f32 v[18:19], v[18:19], v[20:21] neg_lo:[0,1] neg_hi:[0,1]
	v_xor_b32_e32 v20, 0x80000000, v19
	v_mov_b32_e32 v21, v18
	v_pk_add_f32 v[18:19], v[44:45], v[30:31]
	v_pk_add_f32 v[30:31], v[44:45], v[30:31] neg_lo:[0,1] neg_hi:[0,1]
	v_pk_add_f32 v[44:45], v[16:17], v[20:21]
	v_pk_add_f32 v[16:17], v[16:17], v[20:21] neg_lo:[0,1] neg_hi:[0,1]
	v_pk_add_f32 v[20:21], v[46:47], v[78:79]
	ds_write2_b64 v13, v[52:53], v[20:21] offset1:16
	ds_write2_b64 v15, v[70:71], v[22:23] offset0:32 offset1:48
	ds_write2_b64 v51, v[74:75], v[28:29] offset0:64 offset1:80
	ds_write2_b64 v54, v[34:35], v[18:19] offset0:96 offset1:112
	ds_write2_b64 v55, v[94:95], v[86:87] offset0:128 offset1:144
	ds_write2_b64 v56, v[88:89], v[40:41] offset0:160 offset1:176
	ds_write2_b64 v57, v[96:97], v[48:49] offset0:192 offset1:208
	ds_write2_b64 v58, v[84:85], v[44:45] offset0:224 offset1:240
	ds_write2_b64 v59, v[92:93], v[36:37] offset1:16
	ds_write2_b64 v60, v[72:73], v[24:25] offset0:32 offset1:48
	ds_write2_b64 v61, v[90:91], v[42:43] offset0:64 offset1:80
	ds_write2_b64 v62, v[82:83], v[30:31] offset0:96 offset1:112
	ds_write2_b64 v63, v[80:81], v[32:33] offset0:128 offset1:144
	ds_write2_b64 v64, v[76:77], v[26:27] offset0:160 offset1:176
	ds_write2_b64 v65, v[68:69], v[38:39] offset0:192 offset1:208
	ds_write2_b64 v101, v[66:67], v[16:17] offset0:224 offset1:240
	v_mov_b32_e32 v10, v174
	s_waitcnt lgkmcnt(0)
	s_barrier
	v_mov_b32_e32 v58, v180
	v_mov_b32_e32 v59, v181
	v_lshl_add_u32 v10, v10, 3, 0
	ds_read_b64 v[34:35], v10
	ds_read_b64 v[36:37], v10 offset:4224
	ds_read_b64 v[38:39], v10 offset:8448
	ds_read_b64 v[40:41], v10 offset:12672
	ds_read_b64 v[42:43], v10 offset:16896
	ds_read_b64 v[44:45], v10 offset:21120
	ds_read_b64 v[50:51], v10 offset:25344
	ds_read_b64 v[52:53], v10 offset:29568
	ds_read_b64 v[54:55], v10 offset:33792
	ds_read_b64 v[56:57], v10 offset:38016
	ds_read_b64 v[64:65], v10 offset:42240
	ds_read_b64 v[74:75], v10 offset:46464
	ds_read_b64 v[76:77], v10 offset:50688
	ds_read_b64 v[78:79], v10 offset:54912
	ds_read_b64 v[80:81], v10 offset:59136
	ds_read_b64 v[82:83], v10 offset:63360
	v_add_u32_e32 v13, 0x10800, v10
	v_add_u32_e32 v15, 0x11880, v10
	v_add_u32_e32 v16, 0x12900, v10
	v_add_u32_e32 v17, 0x13980, v10
	ds_read_b64 v[84:85], v13
	ds_read_b64 v[86:87], v15
	ds_read_b64 v[88:89], v16
	ds_read_b64 v[92:93], v17
	v_add_u32_e32 v13, 0x14a00, v10
	v_add_u32_e32 v15, 0x15a80, v10
	v_add_u32_e32 v16, 0x16b00, v10
	v_add_u32_e32 v17, 0x17b80, v10
	ds_read_b64 v[96:97], v13
	ds_read_b64 v[98:99], v15
	ds_read_b64 v[94:95], v16
	ds_read_b64 v[90:91], v17
	v_add_u32_e32 v13, 0x18c00, v10
	v_add_u32_e32 v15, 0x19c80, v10
	v_add_u32_e32 v16, 0x1ad00, v10
	v_add_u32_e32 v17, 0x1bd80, v10
	ds_read_b64 v[72:73], v13
	ds_read_b64 v[70:71], v15
	ds_read_b64 v[68:69], v16
	ds_read_b64 v[66:67], v17
	v_add_u32_e32 v13, 0x1ce00, v10
	v_add_u32_e32 v15, 0x1de80, v10
	v_add_u32_e32 v16, 0x1ef00, v10
	v_add_u32_e32 v10, 0x1ff80, v10
	ds_read_b64 v[62:63], v13
	ds_read_b64 v[60:61], v15
	ds_read_b64 v[100:101], v16
	ds_read_b64 v[102:103], v10
	s_mov_b32 s45, s43
	v_mov_b32_e32 v10, v164
	s_lshl_b64 s[0:1], s[44:45], 2
	v_readlane_b32 s2, v251, 40
	s_add_u32 s0, s2, s0
	v_readlane_b32 s2, v251, 46
	v_mov_b32_e32 v24, v165
	v_mov_b32_e32 v32, v166
	v_mov_b32_e32 v28, v167
	v_mov_b32_e32 v46, v168
	v_mov_b32_e32 v48, v169
	v_mov_b32_e32 v30, v170
	v_mov_b32_e32 v26, v171
	v_mov_b32_e32 v10, v172
	v_mov_b32_e32 v16, v184
	v_mov_b32_e32 v19, v185
	s_addc_u32 s1, s2, s1
	s_waitcnt lgkmcnt(0)
	s_barrier
	global_load_dword v13, v11, s[0:1]
	s_and_b64 s[0:1], s[96:97], exec
	s_movk_i32 s0, 0x800
	s_cselect_b32 s2, 0x400, s0
	v_readlane_b32 s20, v251, 36
	s_add_i32 s4, s2, s20
	s_mul_i32 s0, s4, 0x8200
	v_readlane_b32 s3, v250, 23
	s_mul_hi_i32 s1, s4, 0x8200
	s_add_u32 s0, s3, s0
	v_readlane_b32 s3, v251, 20
	s_addc_u32 s1, s3, s1
	s_lshl_b32 s2, s2, 2
	v_mov_b32_e32 v10, s2
	v_readlane_b32 s2, v251, 50
	v_readlane_b32 s3, v251, 51
	v_readlane_b32 s5, v251, 52
	v_readlane_b32 s6, v251, 18
	v_ashrrev_i32_e32 v15, 31, v14
	v_lshl_add_u64 v[22:23], v[14:15], 2, s[72:73]
	v_cmp_lt_i32_e32 vcc, 0, v14
	global_load_dword v189, v10, s[2:3]
	s_add_i32 s2, s4, 0xc00
	s_ashr_i32 s3, s2, 31
	s_lshl_b64 s[2:3], s[2:3], 2
	s_add_u32 s2, s5, s2
	s_addc_u32 s3, s6, s3
	global_load_dword v191, v11, s[2:3]
	s_add_i32 s2, s4, 0x1800
	s_ashr_i32 s3, s2, 31
	s_lshl_b64 s[2:3], s[2:3], 2
	s_add_u32 s2, s5, s2
	s_addc_u32 s3, s6, s3
	global_load_dword v192, v11, s[2:3]
	v_readlane_b32 s2, v251, 42
	v_readlane_b32 s3, v251, 43
	v_mov_b32_e32 v17, 0
	v_lshl_add_u64 v[20:21], v[14:15], 1, s[0:1]
	v_mov_b32_e32 v18, 0
	v_readlane_b32 s21, v251, 37
	s_nop 0
	global_load_dword v193, v10, s[2:3]
	s_nop 0
	v_lshlrev_b32_e32 v234, 1, v14
	v_lshlrev_b32_e32 v235, 2, v14
	v_add_u32_e32 v235, 0x1000, v235
	global_load_dword v190, v235, s[72:73] offset:-4096
	global_load_ushort v195, v234, s[0:1] offset:-2
	global_load_ushort v196, v234, s[0:1]
	global_load_ushort v197, v234, s[0:1] offset:2
	global_load_dword v198, v235, s[66:67] offset:-4096
	global_load_dword v199, v235, s[72:73] offset:-2048
	global_load_ushort v200, v234, s[0:1] offset:1022
	global_load_ushort v201, v234, s[0:1] offset:1024
	global_load_ushort v202, v234, s[0:1] offset:1026
	global_load_dword v203, v235, s[66:67] offset:-2048
	global_load_dword v204, v235, s[72:73]
	global_load_ushort v205, v234, s[0:1] offset:2046
	global_load_ushort v206, v234, s[0:1] offset:2048
	global_load_ushort v207, v234, s[0:1] offset:2050
	global_load_dword v208, v235, s[66:67]
	global_load_dword v209, v235, s[72:73] offset:2048
	global_load_ushort v210, v234, s[0:1] offset:3070
	global_load_ushort v211, v234, s[0:1] offset:3072
	global_load_ushort v212, v234, s[0:1] offset:3074
	global_load_dword v213, v235, s[66:67] offset:2048
	v_lshlrev_b32_e32 v234, 1, v14
	v_add_u32_e32 v234, 0x1000, v234
	v_lshlrev_b32_e32 v235, 2, v14
	v_add_u32_e32 v235, 0x3000, v235
	global_load_dword v214, v235, s[72:73] offset:-4096
	global_load_ushort v215, v234, s[0:1] offset:-2
	global_load_ushort v216, v234, s[0:1]
	global_load_ushort v217, v234, s[0:1] offset:2
	global_load_dword v218, v235, s[66:67] offset:-4096
	global_load_dword v219, v235, s[72:73] offset:-2048
	global_load_ushort v220, v234, s[0:1] offset:1022
	global_load_ushort v221, v234, s[0:1] offset:1024
	global_load_ushort v222, v234, s[0:1] offset:1026
	global_load_dword v223, v235, s[66:67] offset:-2048
	global_load_dword v224, v235, s[72:73]
	global_load_ushort v225, v234, s[0:1] offset:2046
	global_load_ushort v226, v234, s[0:1] offset:2048
	global_load_ushort v227, v234, s[0:1] offset:2050
	global_load_dword v228, v235, s[66:67]
	global_load_dword v229, v235, s[72:73] offset:2048
	global_load_ushort v230, v234, s[0:1] offset:3070
	global_load_ushort v231, v234, s[0:1] offset:3072
	global_load_ushort v232, v234, s[0:1] offset:3074
	global_load_dword v233, v235, s[66:67] offset:2048
	s_waitcnt vmcnt(20)
	v_mov_b32_e32 v10, v190
	s_and_saveexec_b64 s[2:3], vcc
	s_movk_i32 s10, 0x3fff
	s_cbranch_execz .LBB0_2732
	v_mov_b32_e32 v18, v195
	s_nop 0
	v_lshlrev_b32_e32 v18, 16, v18

.LBB0_2734:
	s_or_b64 exec, exec, s[2:3]
	v_add_f32_e32 v6, 0, v6
	v_add_f32_e32 v6, v6, v7
	v_add_f32_e32 v6, v6, v8
	v_add_f32_e32 v6, v6, v9
	v_add_f32_e32 v2, v6, v2
	v_add_f32_e32 v2, v2, v3
	v_add_f32_e32 v2, v2, v4
	v_add_f32_e32 v27, v2, v5
	v_pk_fma_f32 v[2:3], v[58:59], s[92:93], v[58:59] op_sel:[1,0,0] op_sel_hi:[0,1,1]
	v_pk_mul_f32 v[4:5], v[58:59], v[2:3] op_sel:[1,1] op_sel_hi:[0,1] neg_lo:[0,1]
	v_pk_fma_f32 v[4:5], v[58:59], v[2:3], v[4:5] op_sel_hi:[1,0,1]
	s_brev_b32 s6, 28
	v_pk_mul_f32 v[6:7], v[58:59], v[4:5] op_sel:[1,1] op_sel_hi:[0,1] neg_lo:[0,1]
	v_pk_fma_f32 v[6:7], v[58:59], v[4:5], v[6:7] op_sel_hi:[1,0,1]
	v_div_scale_f32 v29, s[4:5], v27, v27, s6
	v_pk_mul_f32 v[8:9], v[58:59], v[6:7] op_sel:[1,1] op_sel_hi:[0,1] neg_lo:[0,1]
	v_pk_fma_f32 v[104:105], v[58:59], v[6:7], v[8:9] op_sel_hi:[1,0,1]
	s_mov_b32 s4, s47
	v_pk_mul_f32 v[8:9], v[58:59], v[104:105] op_sel:[1,1] op_sel_hi:[0,1] neg_lo:[0,1]
	v_pk_fma_f32 v[106:107], v[58:59], v[104:105], v[8:9] op_sel_hi:[1,0,1]
	s_mov_b32 s5, s42
	v_pk_mul_f32 v[8:9], v[58:59], v[106:107] op_sel:[1,1] op_sel_hi:[0,1] neg_lo:[0,1]
	v_pk_fma_f32 v[108:109], v[58:59], v[106:107], v[8:9] op_sel_hi:[1,0,1]
	s_mov_b32 s46, s42
	v_pk_mul_f32 v[8:9], v[58:59], v[108:109] op_sel:[1,1] op_sel_hi:[0,1] neg_lo:[0,1]
	v_pk_fma_f32 v[110:111], v[58:59], v[108:109], v[8:9] op_sel_hi:[1,0,1]
	v_rcp_f32_e32 v31, v29
	v_pk_mul_f32 v[8:9], v[58:59], v[110:111] op_sel:[1,1] op_sel_hi:[0,1] neg_lo:[0,1]
	v_pk_fma_f32 v[112:113], v[58:59], v[110:111], v[8:9] op_sel_hi:[1,0,1]
	v_fma_f32 v33, -v29, v31, 1.0
	v_pk_mul_f32 v[8:9], v[58:59], v[112:113] op_sel:[1,1] op_sel_hi:[0,1] neg_lo:[0,1]
	v_pk_fma_f32 v[114:115], v[58:59], v[112:113], v[8:9] op_sel_hi:[1,0,1]
	v_fmac_f32_e32 v31, v33, v31
	v_pk_mul_f32 v[8:9], v[58:59], v[114:115] op_sel:[1,1] op_sel_hi:[0,1] neg_lo:[0,1]
	v_pk_fma_f32 v[118:119], v[58:59], v[114:115], v[8:9] op_sel_hi:[1,0,1]
	v_div_scale_f32 v33, vcc, s6, v27, s6
	v_pk_mul_f32 v[8:9], v[58:59], v[118:119] op_sel:[1,1] op_sel_hi:[0,1] neg_lo:[0,1]
	v_pk_fma_f32 v[122:123], v[58:59], v[118:119], v[8:9] op_sel_hi:[1,0,1]
	v_mul_f32_e32 v47, v33, v31
	v_pk_mul_f32 v[8:9], v[58:59], v[122:123] op_sel:[1,1] op_sel_hi:[0,1] neg_lo:[0,1]
	v_pk_fma_f32 v[120:121], v[58:59], v[122:123], v[8:9] op_sel_hi:[1,0,1]
	v_fma_f32 v49, -v29, v47, v33
	v_pk_mul_f32 v[8:9], v[58:59], v[120:121] op_sel:[1,1] op_sel_hi:[0,1] neg_lo:[0,1]
	v_pk_fma_f32 v[116:117], v[58:59], v[120:121], v[8:9] op_sel_hi:[1,0,1]
	v_fmac_f32_e32 v47, v49, v31
	v_pk_mul_f32 v[8:9], v[58:59], v[116:117] op_sel:[1,1] op_sel_hi:[0,1] neg_lo:[0,1]
	v_pk_fma_f32 v[124:125], v[58:59], v[116:117], v[8:9] op_sel_hi:[1,0,1]
	v_fma_f32 v29, -v29, v47, v33
	v_pk_mul_f32 v[8:9], v[58:59], v[124:125] op_sel:[1,1] op_sel_hi:[0,1] neg_lo:[0,1]
	v_pk_fma_f32 v[126:127], v[58:59], v[124:125], v[8:9] op_sel_hi:[1,0,1]
	v_div_fmas_f32 v29, v29, v31, v47
	v_pk_mul_f32 v[8:9], v[58:59], v[126:127] op_sel:[1,1] op_sel_hi:[0,1] neg_lo:[0,1]
	v_pk_fma_f32 v[128:129], v[58:59], v[126:127], v[8:9] op_sel_hi:[1,0,1]
	v_div_fixup_f32 v194, v29, v27, s6
	v_pk_mul_f32 v[8:9], v[58:59], v[128:129] op_sel:[1,1] op_sel_hi:[0,1] neg_lo:[0,1]
	v_pk_fma_f32 v[130:131], v[58:59], v[128:129], v[8:9] op_sel_hi:[1,0,1]
	s_xor_b64 s[2:3], s[96:97], -1
	v_pk_mul_f32 v[8:9], v[58:59], v[130:131] op_sel:[1,1] op_sel_hi:[0,1] neg_lo:[0,1]
	v_pk_fma_f32 v[132:133], v[58:59], v[130:131], v[8:9] op_sel_hi:[1,0,1]
	s_mov_b32 s8, 0x3f45e403
	v_pk_mul_f32 v[8:9], v[58:59], v[132:133] op_sel:[1,1] op_sel_hi:[0,1] neg_lo:[0,1]
	v_pk_fma_f32 v[134:135], v[58:59], v[132:133], v[8:9] op_sel_hi:[1,0,1]
	s_mov_b32 s12, 0x3f0e39da
	v_pk_mul_f32 v[8:9], v[58:59], v[134:135] op_sel:[1,1] op_sel_hi:[0,1] neg_lo:[0,1]
	v_pk_fma_f32 v[136:137], v[58:59], v[134:135], v[8:9] op_sel_hi:[1,0,1]
	s_and_b64 vcc, exec, s[2:3]
	v_pk_mul_f32 v[8:9], v[58:59], v[136:137] op_sel:[1,1] op_sel_hi:[0,1] neg_lo:[0,1]
	v_pk_fma_f32 v[138:139], v[58:59], v[136:137], v[8:9] op_sel_hi:[1,0,1]
	s_movk_i32 s45, 0x4000
	v_pk_mul_f32 v[8:9], v[58:59], v[138:139] op_sel:[1,1] op_sel_hi:[0,1] neg_lo:[0,1]
	v_pk_fma_f32 v[140:141], v[58:59], v[138:139], v[8:9] op_sel_hi:[1,0,1]
	s_movk_i32 s50, 0xfc00
	v_pk_mul_f32 v[8:9], v[58:59], v[140:141] op_sel:[1,1] op_sel_hi:[0,1] neg_lo:[0,1]
	v_pk_fma_f32 v[142:143], v[58:59], v[140:141], v[8:9] op_sel_hi:[1,0,1]
	s_movk_i32 s51, 0xfa00
	v_pk_mul_f32 v[8:9], v[58:59], v[142:143] op_sel:[1,1] op_sel_hi:[0,1] neg_lo:[0,1]
	v_pk_fma_f32 v[144:145], v[58:59], v[142:143], v[8:9] op_sel_hi:[1,0,1]
	s_movk_i32 s56, 0xf800
	v_pk_mul_f32 v[8:9], v[58:59], v[144:145] op_sel:[1,1] op_sel_hi:[0,1] neg_lo:[0,1]
	v_pk_fma_f32 v[146:147], v[58:59], v[144:145], v[8:9] op_sel_hi:[1,0,1]
	s_movk_i32 s57, 0xf600
	v_pk_mul_f32 v[8:9], v[58:59], v[146:147] op_sel:[1,1] op_sel_hi:[0,1] neg_lo:[0,1]
	v_pk_fma_f32 v[148:149], v[58:59], v[146:147], v[8:9] op_sel_hi:[1,0,1]
	s_movk_i32 s58, 0xf400
	v_pk_mul_f32 v[8:9], v[58:59], v[148:149] op_sel:[1,1] op_sel_hi:[0,1] neg_lo:[0,1]
	v_pk_fma_f32 v[150:151], v[58:59], v[148:149], v[8:9] op_sel_hi:[1,0,1]
	s_movk_i32 s59, 0xf200
	v_pk_mul_f32 v[8:9], v[58:59], v[150:151] op_sel:[1,1] op_sel_hi:[0,1] neg_lo:[0,1]
	v_pk_fma_f32 v[152:153], v[58:59], v[150:151], v[8:9] op_sel_hi:[1,0,1]
	s_movk_i32 s60, 0xf000
	v_pk_mul_f32 v[8:9], v[58:59], v[152:153] op_sel:[1,1] op_sel_hi:[0,1] neg_lo:[0,1]
	v_pk_fma_f32 v[154:155], v[58:59], v[152:153], v[8:9] op_sel_hi:[1,0,1]
	s_movk_i32 s62, 0xee00
	v_pk_mul_f32 v[8:9], v[58:59], v[154:155] op_sel:[1,1] op_sel_hi:[0,1] neg_lo:[0,1]
	v_pk_fma_f32 v[156:157], v[58:59], v[154:155], v[8:9] op_sel_hi:[1,0,1]
	s_movk_i32 s63, 0xec00
	v_pk_mul_f32 v[8:9], v[58:59], v[156:157] op_sel:[1,1] op_sel_hi:[0,1] neg_lo:[0,1]
	v_pk_fma_f32 v[8:9], v[58:59], v[156:157], v[8:9] op_sel_hi:[1,0,1]
	v_pk_mul_f32 v[58:59], v[102:103], v[8:9] op_sel:[1,1] op_sel_hi:[0,1] neg_hi:[1,0]
	s_movk_i32 s64, 0xea00
	v_pk_fma_f32 v[8:9], v[102:103], v[8:9], v[58:59] op_sel_hi:[1,0,1]
	v_pk_mul_f32 v[58:59], v[100:101], v[156:157] op_sel:[1,1] op_sel_hi:[0,1] neg_hi:[1,0]
	s_movk_i32 s65, 0xe800
	v_pk_fma_f32 v[58:59], v[100:101], v[156:157], v[58:59] op_sel_hi:[1,0,1]
	v_pk_mul_f32 v[100:101], v[60:61], v[154:155] op_sel:[1,1] op_sel_hi:[0,1] neg_hi:[1,0]
	s_mov_b32 s9, 0xbf226799
	v_pk_fma_f32 v[60:61], v[60:61], v[154:155], v[100:101] op_sel_hi:[1,0,1]
	v_pk_mul_f32 v[100:101], v[62:63], v[152:153] op_sel:[1,1] op_sel_hi:[0,1] neg_hi:[1,0]
	s_mov_b32 s13, 0xbf54db31
	v_pk_fma_f32 v[62:63], v[62:63], v[152:153], v[100:101] op_sel_hi:[1,0,1]
	v_pk_mul_f32 v[100:101], v[66:67], v[150:151] op_sel:[1,1] op_sel_hi:[0,1] neg_hi:[1,0]
	s_movk_i32 s11, 0xfe00
	v_pk_fma_f32 v[66:67], v[66:67], v[150:151], v[100:101] op_sel_hi:[1,0,1]
	v_pk_mul_f32 v[100:101], v[68:69], v[148:149] op_sel:[1,1] op_sel_hi:[0,1] neg_hi:[1,0]
	v_pk_fma_f32 v[68:69], v[68:69], v[148:149], v[100:101] op_sel_hi:[1,0,1]
	v_pk_mul_f32 v[100:101], v[70:71], v[146:147] op_sel:[1,1] op_sel_hi:[0,1] neg_hi:[1,0]
	v_pk_fma_f32 v[70:71], v[70:71], v[146:147], v[100:101] op_sel_hi:[1,0,1]
	v_pk_mul_f32 v[100:101], v[72:73], v[144:145] op_sel:[1,1] op_sel_hi:[0,1] neg_hi:[1,0]
	v_pk_fma_f32 v[72:73], v[72:73], v[144:145], v[100:101] op_sel_hi:[1,0,1]
	v_pk_mul_f32 v[100:101], v[90:91], v[142:143] op_sel:[1,1] op_sel_hi:[0,1] neg_hi:[1,0]
	v_pk_fma_f32 v[90:91], v[90:91], v[142:143], v[100:101] op_sel_hi:[1,0,1]
	v_pk_mul_f32 v[100:101], v[94:95], v[140:141] op_sel:[1,1] op_sel_hi:[0,1] neg_hi:[1,0]
	v_pk_fma_f32 v[94:95], v[94:95], v[140:141], v[100:101] op_sel_hi:[1,0,1]
	v_pk_mul_f32 v[100:101], v[98:99], v[138:139] op_sel:[1,1] op_sel_hi:[0,1] neg_hi:[1,0]
	v_pk_fma_f32 v[144:145], v[98:99], v[138:139], v[100:101] op_sel_hi:[1,0,1]
	v_pk_mul_f32 v[98:99], v[96:97], v[136:137] op_sel:[1,1] op_sel_hi:[0,1] neg_hi:[1,0]
	v_pk_fma_f32 v[138:139], v[96:97], v[136:137], v[98:99] op_sel_hi:[1,0,1]
	v_pk_mul_f32 v[96:97], v[92:93], v[134:135] op_sel:[1,1] op_sel_hi:[0,1] neg_hi:[1,0]
	v_pk_fma_f32 v[136:137], v[92:93], v[134:135], v[96:97] op_sel_hi:[1,0,1]
	v_pk_mul_f32 v[92:93], v[88:89], v[132:133] op_sel:[1,1] op_sel_hi:[0,1] neg_hi:[1,0]
	v_pk_fma_f32 v[134:135], v[88:89], v[132:133], v[92:93] op_sel_hi:[1,0,1]
	v_pk_mul_f32 v[88:89], v[86:87], v[130:131] op_sel:[1,1] op_sel_hi:[0,1] neg_hi:[1,0]
	v_pk_fma_f32 v[132:133], v[86:87], v[130:131], v[88:89] op_sel_hi:[1,0,1]
	v_pk_mul_f32 v[86:87], v[84:85], v[128:129] op_sel:[1,1] op_sel_hi:[0,1] neg_hi:[1,0]
	v_pk_fma_f32 v[130:131], v[84:85], v[128:129], v[86:87] op_sel_hi:[1,0,1]
	v_pk_mul_f32 v[84:85], v[82:83], v[126:127] op_sel:[1,1] op_sel_hi:[0,1] neg_hi:[1,0]
	v_mov_b32_e32 v86, v19
	v_pk_fma_f32 v[92:93], v[82:83], v[126:127], v[84:85] op_sel_hi:[1,0,1]
	v_pk_mul_f32 v[82:83], v[80:81], v[124:125] op_sel:[1,1] op_sel_hi:[0,1] neg_hi:[1,0]
	v_pk_mul_f32 v[86:87], v[86:87], s[4:5] op_sel_hi:[0,1] neg_lo:[1,0]
	v_pk_fma_f32 v[96:97], v[80:81], v[124:125], v[82:83] op_sel_hi:[1,0,1]
	v_pk_mul_f32 v[80:81], v[78:79], v[116:117] op_sel:[1,1] op_sel_hi:[0,1] neg_hi:[1,0]
	v_pk_add_f32 v[88:89], v[96:97], v[58:59]
	v_pk_fma_f32 v[116:117], v[78:79], v[116:117], v[80:81] op_sel_hi:[1,0,1]
	v_pk_mul_f32 v[78:79], v[76:77], v[120:121] op_sel:[1,1] op_sel_hi:[0,1] neg_hi:[1,0]
	v_pk_fma_f32 v[86:87], v[16:17], s[46:47], v[86:87] op_sel_hi:[0,1,1]
	v_pk_fma_f32 v[120:121], v[76:77], v[120:121], v[78:79] op_sel_hi:[1,0,1]
	v_pk_mul_f32 v[76:77], v[74:75], v[122:123] op_sel:[1,1] op_sel_hi:[0,1] neg_hi:[1,0]
	v_pk_add_f32 v[78:79], v[92:93], v[8:9]
	v_pk_fma_f32 v[122:123], v[74:75], v[122:123], v[76:77] op_sel_hi:[1,0,1]
	v_pk_mul_f32 v[74:75], v[64:65], v[118:119] op_sel:[1,1] op_sel_hi:[0,1] neg_hi:[1,0]
	s_mov_b64 s[4:5], -1
	v_pk_fma_f32 v[124:125], v[64:65], v[118:119], v[74:75] op_sel_hi:[1,0,1]
	v_pk_mul_f32 v[64:65], v[56:57], v[114:115] op_sel:[1,1] op_sel_hi:[0,1] neg_hi:[1,0]
	v_pk_fma_f32 v[126:127], v[56:57], v[114:115], v[64:65] op_sel_hi:[1,0,1]
	v_pk_mul_f32 v[56:57], v[54:55], v[112:113] op_sel:[1,1] op_sel_hi:[0,1] neg_hi:[1,0]
	v_pk_add_f32 v[118:119], v[126:127], v[70:71]
	v_pk_fma_f32 v[128:129], v[54:55], v[112:113], v[56:57] op_sel_hi:[1,0,1]
	v_pk_mul_f32 v[54:55], v[52:53], v[110:111] op_sel:[1,1] op_sel_hi:[0,1] neg_hi:[1,0]
	v_pk_add_f32 v[114:115], v[128:129], v[72:73]
	v_pk_fma_f32 v[140:141], v[52:53], v[110:111], v[54:55] op_sel_hi:[1,0,1]
	v_pk_mul_f32 v[52:53], v[50:51], v[108:109] op_sel:[1,1] op_sel_hi:[0,1] neg_hi:[1,0]
	v_pk_add_f32 v[64:65], v[140:141], v[90:91]
	v_pk_fma_f32 v[142:143], v[50:51], v[108:109], v[52:53] op_sel_hi:[1,0,1]
	v_pk_mul_f32 v[50:51], v[44:45], v[106:107] op_sel:[1,1] op_sel_hi:[0,1] neg_hi:[1,0]
	v_pk_add_f32 v[74:75], v[142:143], v[94:95]
	v_pk_fma_f32 v[146:147], v[44:45], v[106:107], v[50:51] op_sel_hi:[1,0,1]
	v_pk_mul_f32 v[44:45], v[42:43], v[104:105] op_sel:[1,1] op_sel_hi:[0,1] neg_hi:[1,0]
	v_pk_add_f32 v[76:77], v[146:147], v[144:145]
	v_pk_fma_f32 v[148:149], v[42:43], v[104:105], v[44:45] op_sel_hi:[1,0,1]
	v_pk_mul_f32 v[42:43], v[40:41], v[6:7] op_sel:[1,1] op_sel_hi:[0,1] neg_hi:[1,0]
	v_pk_add_f32 v[80:81], v[148:149], v[138:139]
	v_pk_fma_f32 v[150:151], v[40:41], v[6:7], v[42:43] op_sel_hi:[1,0,1]
	v_pk_mul_f32 v[6:7], v[38:39], v[4:5] op_sel:[1,1] op_sel_hi:[0,1] neg_hi:[1,0]
	v_pk_add_f32 v[104:105], v[150:151], v[136:137]
	v_pk_fma_f32 v[152:153], v[38:39], v[4:5], v[6:7] op_sel_hi:[1,0,1]
	v_pk_mul_f32 v[4:5], v[2:3], v[36:37] op_sel:[1,1] op_sel_hi:[1,0] neg_hi:[0,1]
	v_pk_add_f32 v[102:103], v[152:153], v[134:135]
	v_pk_fma_f32 v[154:155], v[36:37], v[2:3], v[4:5] op_sel_hi:[1,0,1]
	v_pk_fma_f32 v[156:157], v[34:35], 0, v[34:35] op_sel:[1,0,0] op_sel_hi:[0,0,1] neg_hi:[1,0,0]
	v_pk_add_f32 v[100:101], v[154:155], v[132:133]
	v_pk_add_f32 v[98:99], v[156:157], v[130:131]
	v_pk_add_f32 v[112:113], v[124:125], v[68:69]
	v_pk_add_f32 v[110:111], v[122:123], v[66:67]
	v_pk_add_f32 v[106:107], v[120:121], v[62:63]
	v_pk_add_f32 v[108:109], v[116:117], v[60:61]
	v_pk_add_f32 v[40:41], v[98:99], v[114:115]
	v_pk_add_f32 v[42:43], v[100:101], v[118:119]
	v_pk_add_f32 v[36:37], v[102:103], v[112:113]
	v_pk_add_f32 v[34:35], v[104:105], v[110:111]
	v_pk_add_f32 v[82:83], v[80:81], v[106:107]
	v_pk_add_f32 v[84:85], v[76:77], v[108:109]
	v_pk_add_f32 v[44:45], v[74:75], v[88:89]
	v_pk_add_f32 v[38:39], v[64:65], v[78:79]
	v_pk_add_f32 v[50:51], v[40:41], v[82:83]
	v_pk_add_f32 v[52:53], v[42:43], v[84:85]
	v_pk_add_f32 v[54:55], v[36:37], v[44:45]
	v_pk_add_f32 v[56:57], v[34:35], v[38:39]
	v_pk_add_f32 v[4:5], v[50:51], v[54:55]
	v_pk_add_f32 v[6:7], v[52:53], v[56:57]
	v_pk_add_f32 v[2:3], v[4:5], v[6:7]
	v_pk_mul_f32 v[2:3], v[86:87], v[2:3]
	v_lshl_add_u64 v[86:87], v[14:15], 1, s[54:55]
	s_nop 0
	v_add_f32_e32 v2, v10, v2
	v_add_f32_e32 v10, v3, v2
	s_nop 0
	v_lshlrev_b32_e32 v2, 16, v25
	v_mul_f32_e32 v2, v191, v2
	v_fmac_f32_e32 v2, v189, v18
	v_fmac_f32_e32 v2, v192, v17
	v_add_f32_e32 v17, v193, v2
	v_lshl_add_u64 v[2:3], v[14:15], 2, s[66:67]
	v_mov_b32_e32 v18, v198
	s_nop 0
	v_mul_f32_e32 v18, v13, v18
	v_fmac_f32_e32 v18, v194, v10
	v_mul_f32_e32 v10, v17, v18
	s_cbranch_vccz .LBB0_2736
	v_bfe_u32 v15, v10, 16, 1
	v_add3_u32 v15, v10, v15, s33
	global_store_short_d16_hi v[86:87], v15, off
	s_mov_b64 s[4:5], 0

.LBB0_2742:
	s_or_b64 exec, exec, s[4:5]
	v_pk_add_f32 v[134:135], v[152:153], v[134:135] neg_lo:[0,1] neg_hi:[0,1]
	v_pk_add_f32 v[144:145], v[146:147], v[144:145] neg_lo:[0,1] neg_hi:[0,1]
	s_nop 0
	v_pk_mul_f32 v[152:153], v[30:31], v[134:135] op_sel:[0,1] op_sel_hi:[0,0] neg_lo:[0,1]
	v_pk_fma_f32 v[134:135], v[32:33], v[134:135], v[152:153] op_sel_hi:[0,1,1]
	v_mov_b32_e32 v33, v203
	v_pk_add_f32 v[138:139], v[148:149], v[138:139] neg_lo:[0,1] neg_hi:[0,1]
	v_pk_mul_f32 v[146:147], v[28:29], v[144:145] op_sel:[0,1] op_sel_hi:[0,0] neg_lo:[0,1]
	v_pk_add_f32 v[72:73], v[128:129], v[72:73] neg_lo:[0,1] neg_hi:[0,1]
	v_pk_add_f32 v[70:71], v[126:127], v[70:71] neg_lo:[0,1] neg_hi:[0,1]
	v_pk_fma_f32 v[144:145], v[48:49], v[144:145], v[146:147] op_sel_hi:[0,1,1]
	v_xor_b32_e32 v146, 0x80000000, v73
	v_mov_b32_e32 v147, v72
	v_pk_mul_f32 v[148:149], v[46:47], v[138:139] op_sel:[0,1] op_sel_hi:[0,0] neg_lo:[0,1]
	v_pk_mul_f32 v[72:73], v[24:25], v[70:71] op_sel:[0,1] op_sel_hi:[0,0] neg_lo:[0,1]
	v_pk_add_f32 v[68:69], v[124:125], v[68:69] neg_lo:[0,1] neg_hi:[0,1]
	v_pk_fma_f32 v[138:139], v[46:47], v[138:139], v[148:149] op_sel_hi:[0,1,1]
	v_pk_fma_f32 v[148:149], v[26:27], v[70:71], v[72:73] op_sel_hi:[0,1,1] neg_lo:[1,0,0] neg_hi:[1,0,0]
	v_pk_add_f32 v[136:137], v[150:151], v[136:137] neg_lo:[0,1] neg_hi:[0,1]
	v_pk_add_f32 v[66:67], v[122:123], v[66:67] neg_lo:[0,1] neg_hi:[0,1]
	v_pk_mul_f32 v[150:151], v[48:49], v[136:137] op_sel:[0,1] op_sel_hi:[0,0] neg_lo:[0,1]
	v_pk_add_f32 v[62:63], v[120:121], v[62:63] neg_lo:[0,1] neg_hi:[0,1]
	v_pk_fma_f32 v[136:137], v[28:29], v[136:137], v[150:151] op_sel_hi:[0,1,1]
	v_pk_add_f32 v[132:133], v[154:155], v[132:133] neg_lo:[0,1] neg_hi:[0,1]
	v_pk_add_f32 v[60:61], v[116:117], v[60:61] neg_lo:[0,1] neg_hi:[0,1]
	v_pk_mul_f32 v[154:155], v[26:27], v[132:133] op_sel:[0,1] op_sel_hi:[0,0] neg_lo:[0,1]
	v_pk_add_f32 v[94:95], v[142:143], v[94:95] neg_lo:[0,1] neg_hi:[0,1]
	v_pk_fma_f32 v[132:133], v[24:25], v[132:133], v[154:155] op_sel_hi:[0,1,1]
	v_pk_add_f32 v[90:91], v[140:141], v[90:91] neg_lo:[0,1] neg_hi:[0,1]
	v_pk_add_f32 v[8:9], v[92:93], v[8:9] neg_lo:[0,1] neg_hi:[0,1]
	v_pk_add_f32 v[130:131], v[156:157], v[130:131] neg_lo:[0,1] neg_hi:[0,1]
	v_pk_add_f32 v[92:93], v[132:133], v[148:149]
	v_xor_b32_e32 v18, 0x80000000, v19
	s_mov_b32 s4, s69
	s_mov_b32 s5, s68
	v_mov_b32_e32 v17, v16
	s_andn2_b64 vcc, exec, s[2:3]
	s_nop 0
	v_pk_mul_f32 v[70:71], v[32:33], v[68:69] op_sel:[0,1] op_sel_hi:[0,0] neg_lo:[0,1]
	v_pk_fma_f32 v[124:125], v[30:31], v[68:69], v[70:71] op_sel_hi:[0,1,1] neg_lo:[1,0,0] neg_hi:[1,0,0]
	v_pk_mul_f32 v[68:69], v[28:29], v[66:67] op_sel:[0,1] op_sel_hi:[0,0] neg_lo:[0,1]
	v_pk_fma_f32 v[150:151], v[48:49], v[66:67], v[68:69] op_sel_hi:[0,1,1] neg_lo:[1,0,0] neg_hi:[1,0,0]
	v_pk_mul_f32 v[66:67], v[46:47], v[62:63] op_sel:[0,1] op_sel_hi:[0,0] neg_lo:[0,1]
	v_pk_fma_f32 v[152:153], v[46:47], v[62:63], v[66:67] op_sel_hi:[0,1,1] neg_lo:[1,0,0] neg_hi:[1,0,0]
	v_xor_b32_e32 v62, 0x80000000, v61
	v_mov_b32_e32 v63, v60
	v_pk_mul_f32 v[48:49], v[48:49], v[62:63] op_sel_hi:[0,1]
	v_pk_fma_f32 v[154:155], v[28:29], v[60:61], v[48:49] op_sel_hi:[0,1,1] neg_lo:[1,0,0] neg_hi:[1,0,0]
	v_pk_add_f32 v[28:29], v[96:97], v[58:59] neg_lo:[0,1] neg_hi:[0,1]
	v_pk_mul_f32 v[142:143], v[32:33], v[94:95] op_sel:[0,1] op_sel_hi:[0,0] neg_lo:[0,1]
	v_pk_fma_f32 v[142:143], v[30:31], v[94:95], v[142:143] op_sel_hi:[0,1,1]
	v_pk_mul_f32 v[48:49], v[30:31], v[28:29] op_sel:[0,1] op_sel_hi:[0,0] neg_lo:[0,1]
	v_pk_mul_f32 v[94:95], v[24:25], v[90:91] op_sel:[0,1] op_sel_hi:[0,0] neg_lo:[0,1]
	v_pk_fma_f32 v[156:157], v[32:33], v[28:29], v[48:49] op_sel_hi:[0,1,1] neg_lo:[1,0,0] neg_hi:[1,0,0]
	v_pk_fma_f32 v[140:141], v[26:27], v[90:91], v[94:95] op_sel_hi:[0,1,1]
	v_pk_mul_f32 v[26:27], v[26:27], v[8:9] op_sel:[0,1] op_sel_hi:[0,0] neg_lo:[0,1]
	v_pk_fma_f32 v[158:159], v[24:25], v[8:9], v[26:27] op_sel_hi:[0,1,1] neg_lo:[1,0,0] neg_hi:[1,0,0]
	v_pk_add_f32 v[90:91], v[130:131], v[146:147]
	v_pk_add_f32 v[94:95], v[134:135], v[124:125]
	v_pk_add_f32 v[96:97], v[136:137], v[150:151]
	v_pk_add_f32 v[126:127], v[138:139], v[152:153]
	v_pk_add_f32 v[128:129], v[144:145], v[154:155]
	v_pk_add_f32 v[122:123], v[142:143], v[156:157]
	v_pk_add_f32 v[116:117], v[140:141], v[158:159]
	v_pk_add_f32 v[66:67], v[90:91], v[126:127]
	v_pk_add_f32 v[68:69], v[92:93], v[128:129]
	v_pk_add_f32 v[70:71], v[94:95], v[122:123]
	v_pk_add_f32 v[72:73], v[96:97], v[116:117]
	v_pk_add_f32 v[26:27], v[66:67], v[70:71]
	v_pk_add_f32 v[28:29], v[68:69], v[72:73]
	v_pk_mul_f32 v[48:49], v[18:19], s[4:5]
	v_pk_add_f32 v[8:9], v[26:27], v[28:29]
	v_pk_fma_f32 v[48:49], v[16:17], s[68:69], v[48:49]
	v_pk_mul_f32 v[8:9], v[48:49], v[8:9]
	v_add_f32_e32 v8, v8, v25
	v_add_f32_e32 v8, v9, v8
	v_lshlrev_b32_e32 v9, 16, v31
	v_mul_f32_e32 v9, v191, v9
	v_fmac_f32_e32 v9, v189, v10
	v_fmac_f32_e32 v9, v192, v15
	v_mul_f32_e32 v10, v13, v33
	v_add_f32_e32 v9, v193, v9
	v_fmac_f32_e32 v10, v194, v8
	v_mul_f32_e32 v8, v9, v10
	v_cndmask_b32_e64 v9, 0, 1, s[2:3]
	v_cmp_ne_u32_e64 s[4:5], 1, v9
	s_mov_b64 s[2:3], -1
	s_cbranch_vccnz .LBB0_2744
	v_bfe_u32 v9, v8, 16, 1
	v_add3_u32 v9, v8, v9, s33
	s_mov_b64 s[2:3], 0
	global_store_short_d16_hi v[86:87], v9, off offset:1024

.LBB0_2750:
	s_or_b64 exec, exec, s[2:3]
	v_pk_add_f32 v[8:9], v[100:101], v[118:119] neg_lo:[0,1] neg_hi:[0,1]
	v_mov_b32_e32 v31, v30
	v_mov_b32_e32 v33, v32
	v_pk_mul_f32 v[24:25], v[30:31], v[8:9] op_sel:[0,1] op_sel_hi:[1,0] neg_lo:[0,1]
	v_mov_b32_e32 v47, v46
	v_pk_fma_f32 v[100:101], v[32:33], v[8:9], v[24:25]
	v_pk_add_f32 v[8:9], v[102:103], v[112:113] neg_lo:[0,1] neg_hi:[0,1]
	v_xor_b32_e32 v162, 0x80000000, v30
	v_pk_mul_f32 v[24:25], v[46:47], v[8:9] op_sel:[0,1] op_sel_hi:[1,0] neg_lo:[0,1]
	v_mov_b32_e32 v163, v162
	v_pk_fma_f32 v[102:103], v[46:47], v[8:9], v[24:25]
	v_pk_add_f32 v[8:9], v[104:105], v[110:111] neg_lo:[0,1] neg_hi:[0,1]
	v_xor_b32_e32 v48, 0x80000000, v46
	v_pk_mul_f32 v[24:25], v[32:33], v[8:9] op_sel:[0,1] op_sel_hi:[1,0] neg_lo:[0,1]
	v_mov_b32_e32 v49, v48
	v_pk_fma_f32 v[104:105], v[30:31], v[8:9], v[24:25]
	v_pk_add_f32 v[8:9], v[80:81], v[106:107] neg_lo:[0,1] neg_hi:[0,1]
	v_xor_b32_e32 v160, 0x80000000, v32
	v_xor_b32_e32 v106, 0x80000000, v9
	v_mov_b32_e32 v107, v8
	v_pk_add_f32 v[8:9], v[76:77], v[108:109] neg_lo:[0,1] neg_hi:[0,1]
	v_mov_b32_e32 v161, v160
	v_pk_mul_f32 v[24:25], v[32:33], v[8:9] op_sel:[0,1] op_sel_hi:[1,0] neg_lo:[0,1]
	v_pk_add_f32 v[98:99], v[98:99], v[114:115] neg_lo:[0,1] neg_hi:[0,1]
	v_pk_fma_f32 v[108:109], v[162:163], v[8:9], v[24:25]
	v_pk_add_f32 v[8:9], v[74:75], v[88:89] neg_lo:[0,1] neg_hi:[0,1]
	v_pk_add_f32 v[58:59], v[98:99], v[106:107]
	v_pk_mul_f32 v[24:25], v[46:47], v[8:9] op_sel:[0,1] op_sel_hi:[1,0] neg_lo:[0,1]
	v_pk_add_f32 v[60:61], v[100:101], v[108:109]
	v_pk_fma_f32 v[110:111], v[48:49], v[8:9], v[24:25]
	v_pk_add_f32 v[8:9], v[64:65], v[78:79] neg_lo:[0,1] neg_hi:[0,1]
	v_pk_add_f32 v[62:63], v[102:103], v[110:111]
	v_pk_mul_f32 v[24:25], v[30:31], v[8:9] op_sel:[0,1] op_sel_hi:[1,0] neg_lo:[0,1]
	s_mov_b32 s2, s71
	v_pk_fma_f32 v[112:113], v[160:161], v[8:9], v[24:25]
	s_mov_b32 s3, s70
	v_pk_add_f32 v[64:65], v[104:105], v[112:113]
	v_pk_add_f32 v[8:9], v[58:59], v[62:63]
	v_pk_add_f32 v[24:25], v[60:61], v[64:65]
	v_pk_mul_f32 v[76:77], v[18:19], s[2:3]
	v_pk_add_f32 v[74:75], v[8:9], v[24:25]
	v_pk_fma_f32 v[76:77], v[16:17], s[70:71], v[76:77]
	s_mov_b64 s[2:3], -1
	v_pk_mul_f32 v[74:75], v[76:77], v[74:75]
	v_add_f32_e32 v74, v74, v120
	v_add_f32_e32 v76, v75, v74
	s_nop 0
	v_lshlrev_b32_e32 v74, 16, v121
	v_mul_f32_e32 v74, v191, v74
	v_fmac_f32_e32 v74, v189, v10
	v_fmac_f32_e32 v74, v192, v15
	v_add_f32_e32 v10, v193, v74
	v_add_co_u32_e32 v74, vcc, 0x1000, v2
	s_nop 1
	v_addc_co_u32_e32 v75, vcc, 0, v3, vcc
	v_mov_b32_e32 v15, v208
	s_and_b64 vcc, exec, s[4:5]
	s_nop 0
	v_mul_f32_e32 v15, v13, v15
	v_fmac_f32_e32 v15, v194, v76
	v_mul_f32_e32 v10, v10, v15
	s_cbranch_vccnz .LBB0_2752
	v_bfe_u32 v15, v10, 16, 1
	v_add3_u32 v15, v10, v15, s33
	s_mov_b64 s[2:3], 0
	global_store_short_d16_hi v[86:87], v15, off offset:2048

.LBB0_2758:
	s_or_b64 exec, exec, s[2:3]
	v_pk_add_f32 v[74:75], v[132:133], v[148:149] neg_lo:[0,1] neg_hi:[0,1]
	v_pk_add_f32 v[114:115], v[130:131], v[146:147] neg_lo:[0,1] neg_hi:[0,1]
	v_pk_mul_f32 v[76:77], v[30:31], v[74:75] op_sel:[0,1] op_sel_hi:[1,0] neg_lo:[0,1]
	s_mov_b32 s2, s41
	v_pk_fma_f32 v[118:119], v[32:33], v[74:75], v[76:77]
	v_pk_add_f32 v[74:75], v[134:135], v[124:125] neg_lo:[0,1] neg_hi:[0,1]
	s_mov_b32 s3, s40
	v_pk_mul_f32 v[76:77], v[46:47], v[74:75] op_sel:[0,1] op_sel_hi:[1,0] neg_lo:[0,1]
	v_pk_fma_f32 v[120:121], v[46:47], v[74:75], v[76:77]
	v_pk_add_f32 v[74:75], v[136:137], v[150:151] neg_lo:[0,1] neg_hi:[0,1]
	v_pk_mul_f32 v[76:77], v[32:33], v[74:75] op_sel:[0,1] op_sel_hi:[1,0] neg_lo:[0,1]
	v_pk_fma_f32 v[124:125], v[30:31], v[74:75], v[76:77]
	v_pk_add_f32 v[74:75], v[138:139], v[152:153] neg_lo:[0,1] neg_hi:[0,1]
	v_xor_b32_e32 v130, 0x80000000, v75
	v_mov_b32_e32 v131, v74
	v_pk_add_f32 v[74:75], v[144:145], v[154:155] neg_lo:[0,1] neg_hi:[0,1]
	v_pk_mul_f32 v[32:33], v[32:33], v[74:75] op_sel:[0,1] op_sel_hi:[1,0] neg_lo:[0,1]
	v_pk_fma_f32 v[132:133], v[162:163], v[74:75], v[32:33]
	v_pk_add_f32 v[32:33], v[142:143], v[156:157] neg_lo:[0,1] neg_hi:[0,1]
	v_pk_add_f32 v[76:77], v[118:119], v[132:133]
	v_pk_mul_f32 v[74:75], v[46:47], v[32:33] op_sel:[0,1] op_sel_hi:[1,0] neg_lo:[0,1]
	v_pk_fma_f32 v[134:135], v[48:49], v[32:33], v[74:75]
	v_pk_add_f32 v[32:33], v[140:141], v[158:159] neg_lo:[0,1] neg_hi:[0,1]
	v_pk_add_f32 v[78:79], v[120:121], v[134:135]
	v_pk_mul_f32 v[30:31], v[30:31], v[32:33] op_sel:[0,1] op_sel_hi:[1,0] neg_lo:[0,1]
	v_pk_add_f32 v[74:75], v[114:115], v[130:131]
	v_pk_fma_f32 v[136:137], v[160:161], v[32:33], v[30:31]
	v_pk_add_f32 v[30:31], v[74:75], v[78:79]
	v_pk_add_f32 v[80:81], v[124:125], v[136:137]
	v_pk_mul_f32 v[140:141], v[18:19], s[2:3]
	v_pk_add_f32 v[32:33], v[76:77], v[80:81]
	v_pk_fma_f32 v[140:141], v[16:17], s[40:41], v[140:141]
	v_pk_add_f32 v[138:139], v[30:31], v[32:33]
	s_mov_b64 s[2:3], -1
	v_pk_mul_f32 v[138:139], v[140:141], v[138:139]
	v_add_f32_e32 v88, v138, v88
	v_add_f32_e32 v138, v139, v88
	s_nop 0
	v_lshlrev_b32_e32 v88, 16, v89
	v_mul_f32_e32 v88, v191, v88
	v_fmac_f32_e32 v88, v189, v10
	v_fmac_f32_e32 v88, v192, v15
	v_add_f32_e32 v10, v193, v88
	v_add_co_u32_e32 v88, vcc, 0x1000, v2
	s_nop 1
	v_addc_co_u32_e32 v89, vcc, 0, v3, vcc
	v_mov_b32_e32 v15, v213
	s_and_b64 vcc, exec, s[4:5]
	s_nop 0
	v_mul_f32_e32 v15, v13, v15
	v_fmac_f32_e32 v15, v194, v138
	v_mul_f32_e32 v10, v10, v15
	s_cbranch_vccnz .LBB0_2760
	v_bfe_u32 v15, v10, 16, 1
	v_add3_u32 v15, v10, v15, s33
	s_mov_b64 s[2:3], 0
	global_store_short_d16_hi v[86:87], v15, off offset:3072

.LBB0_2766:
	s_or_b64 exec, exec, s[2:3]
	v_pk_add_f32 v[82:83], v[40:41], v[82:83] neg_lo:[0,1] neg_hi:[0,1]
	v_pk_add_f32 v[40:41], v[42:43], v[84:85] neg_lo:[0,1] neg_hi:[0,1]
	v_pk_add_f32 v[36:37], v[36:37], v[44:45] neg_lo:[0,1] neg_hi:[0,1]
	v_pk_add_f32 v[34:35], v[34:35], v[38:39] neg_lo:[0,1] neg_hi:[0,1]
	v_xor_b32_e32 v86, 0x80000000, v37
	v_mov_b32_e32 v87, v36
	v_pk_mul_f32 v[42:43], v[46:47], v[40:41] op_sel:[0,1] op_sel_hi:[1,0] neg_lo:[0,1]
	v_pk_mul_f32 v[36:37], v[46:47], v[34:35] op_sel:[0,1] op_sel_hi:[1,0] neg_lo:[0,1]
	v_pk_fma_f32 v[84:85], v[46:47], v[40:41], v[42:43]
	v_pk_fma_f32 v[88:89], v[48:49], v[34:35], v[36:37]
	s_mov_b32 s2, s95
	s_mov_b32 s3, s94
	v_pk_add_f32 v[34:35], v[82:83], v[86:87]
	v_pk_add_f32 v[36:37], v[84:85], v[88:89]
	v_pk_mul_f32 v[40:41], v[18:19], s[2:3]
	v_pk_add_f32 v[38:39], v[34:35], v[36:37]
	v_pk_fma_f32 v[40:41], v[16:17], s[94:95], v[40:41]
	s_mov_b64 s[2:3], -1
	v_pk_mul_f32 v[38:39], v[40:41], v[38:39]
	v_add_f32_e32 v10, v38, v10
	s_nop 0
	v_lshlrev_b32_e32 v38, 16, v141
	v_mul_f32_e32 v38, v191, v38
	v_fmac_f32_e32 v38, v189, v140
	v_fmac_f32_e32 v38, v192, v15
	v_add_f32_e32 v15, v193, v38
	v_add_co_u32_e32 v38, vcc, 0x2000, v2
	v_add_f32_e32 v10, v39, v10
	s_nop 0
	v_addc_co_u32_e32 v39, vcc, 0, v3, vcc
	v_mov_b32_e32 v38, v218
	s_and_b64 vcc, exec, s[4:5]
	s_nop 0
	v_mul_f32_e32 v38, v13, v38
	v_fmac_f32_e32 v38, v194, v10
	v_mul_f32_e32 v10, v15, v38
	s_cbranch_vccnz .LBB0_2768
	v_bfe_u32 v15, v10, 16, 1
	v_add3_u32 v15, v10, v15, s33
	v_lshl_add_u64 v[38:39], v[138:139], 1, s[54:55]
	s_mov_b64 s[2:3], 0
	global_store_short_d16_hi v[38:39], v15, off

.LBB0_2782:
	s_or_b64 exec, exec, s[2:3]
	v_pk_add_f32 v[42:43], v[100:101], v[108:109] neg_lo:[0,1] neg_hi:[0,1]
	v_pk_add_f32 v[98:99], v[98:99], v[106:107] neg_lo:[0,1] neg_hi:[0,1]
	v_pk_mul_f32 v[44:45], v[46:47], v[42:43] op_sel:[0,1] op_sel_hi:[1,0] neg_lo:[0,1]
	s_mov_b32 s2, s81
	v_pk_fma_f32 v[100:101], v[46:47], v[42:43], v[44:45]
	v_pk_add_f32 v[42:43], v[102:103], v[110:111] neg_lo:[0,1] neg_hi:[0,1]
	s_mov_b32 s3, s80
	v_xor_b32_e32 v102, 0x80000000, v43
	v_mov_b32_e32 v103, v42
	v_pk_add_f32 v[42:43], v[104:105], v[112:113] neg_lo:[0,1] neg_hi:[0,1]
	v_pk_mul_f32 v[108:109], v[18:19], s[2:3]
	v_pk_mul_f32 v[44:45], v[46:47], v[42:43] op_sel:[0,1] op_sel_hi:[1,0] neg_lo:[0,1]
	v_pk_fma_f32 v[108:109], v[16:17], s[80:81], v[108:109]
	v_pk_fma_f32 v[104:105], v[48:49], v[42:43], v[44:45]
	v_pk_add_f32 v[42:43], v[98:99], v[102:103]
	v_pk_add_f32 v[44:45], v[100:101], v[104:105]
	s_mov_b64 s[2:3], -1
	v_pk_add_f32 v[106:107], v[42:43], v[44:45]
	v_pk_mul_f32 v[106:107], v[108:109], v[106:107]
	v_add_f32_e32 v10, v106, v10
	s_nop 0
	v_lshlrev_b32_e32 v106, 16, v123
	v_mul_f32_e32 v106, v191, v106
	v_fmac_f32_e32 v106, v189, v122
	v_fmac_f32_e32 v106, v192, v15
	v_add_f32_e32 v15, v193, v106
	v_add_co_u32_e32 v106, vcc, 0x3000, v2
	v_add_f32_e32 v10, v107, v10
	s_nop 0
	v_addc_co_u32_e32 v107, vcc, 0, v3, vcc
	v_mov_b32_e32 v106, v228
	s_and_b64 vcc, exec, s[4:5]
	s_nop 0
	v_mul_f32_e32 v106, v13, v106
	v_fmac_f32_e32 v106, v194, v10
	v_mul_f32_e32 v10, v15, v106
	s_cbranch_vccnz .LBB0_2784
	v_bfe_u32 v15, v10, 16, 1
	v_add3_u32 v15, v10, v15, s33
	v_lshl_add_u64 v[106:107], v[116:117], 1, s[54:55]
	s_mov_b64 s[2:3], 0
	global_store_short_d16_hi v[106:107], v15, off

.LBB0_2790:
	s_or_b64 exec, exec, s[2:3]
	v_pk_add_f32 v[108:109], v[118:119], v[132:133] neg_lo:[0,1] neg_hi:[0,1]
	v_pk_add_f32 v[112:113], v[120:121], v[134:135] neg_lo:[0,1] neg_hi:[0,1]
	v_pk_mul_f32 v[110:111], v[46:47], v[108:109] op_sel:[0,1] op_sel_hi:[1,0] neg_lo:[0,1]
	v_pk_add_f32 v[106:107], v[114:115], v[130:131] neg_lo:[0,1] neg_hi:[0,1]
	v_pk_fma_f32 v[108:109], v[46:47], v[108:109], v[110:111]
	v_xor_b32_e32 v110, 0x80000000, v113
	v_mov_b32_e32 v111, v112
	v_pk_add_f32 v[112:113], v[124:125], v[136:137] neg_lo:[0,1] neg_hi:[0,1]
	s_mov_b32 s2, s9
	v_pk_mul_f32 v[46:47], v[46:47], v[112:113] op_sel:[0,1] op_sel_hi:[1,0] neg_lo:[0,1]
	s_mov_b32 s3, s8
	v_pk_fma_f32 v[112:113], v[48:49], v[112:113], v[46:47]
	v_pk_add_f32 v[46:47], v[106:107], v[110:111]
	v_pk_add_f32 v[48:49], v[108:109], v[112:113]
	v_pk_mul_f32 v[118:119], v[18:19], s[2:3]
	v_pk_add_f32 v[114:115], v[46:47], v[48:49]
	v_pk_fma_f32 v[118:119], v[16:17], s[8:9], v[118:119]
	s_mov_b64 s[2:3], -1
	v_pk_mul_f32 v[114:115], v[118:119], v[114:115]
	v_add_f32_e32 v10, v114, v10
	s_nop 0
	v_lshlrev_b32_e32 v114, 16, v123
	v_mul_f32_e32 v114, v191, v114
	v_fmac_f32_e32 v114, v189, v122
	v_fmac_f32_e32 v114, v192, v15
	v_add_f32_e32 v15, v193, v114
	v_add_co_u32_e32 v114, vcc, 0x3000, v2
	v_add_f32_e32 v10, v115, v10
	s_nop 0
	v_addc_co_u32_e32 v115, vcc, 0, v3, vcc
	v_mov_b32_e32 v114, v233
	s_and_b64 vcc, exec, s[4:5]
	s_nop 0
	v_mul_f32_e32 v114, v13, v114
	v_fmac_f32_e32 v114, v194, v10
	v_mul_f32_e32 v10, v15, v114
	s_cbranch_vccnz .LBB0_2792
	v_bfe_u32 v15, v10, 16, 1
	v_add3_u32 v15, v10, v15, s33
	v_lshl_add_u64 v[114:115], v[116:117], 1, s[54:55]
	s_mov_b64 s[2:3], 0
	global_store_short_d16_hi v[114:115], v15, off

.LBB0_2798:
	s_or_b64 exec, exec, s[2:3]
	v_pk_add_f32 v[50:51], v[50:51], v[54:55] neg_lo:[0,1] neg_hi:[0,1]
	v_pk_add_f32 v[54:55], v[52:53], v[56:57] neg_lo:[0,1] neg_hi:[0,1]
	s_mov_b32 s2, s53
	s_mov_b32 s3, s52
	v_xor_b32_e32 v52, 0x80000000, v55
	v_mov_b32_e32 v53, v54
	v_pk_mul_f32 v[56:57], v[18:19], s[2:3]
	v_pk_add_f32 v[54:55], v[50:51], v[52:53]
	v_pk_fma_f32 v[56:57], v[16:17], s[52:53], v[56:57]
	s_mov_b64 s[2:3], -1
	v_pk_mul_f32 v[54:55], v[56:57], v[54:55]
	v_add_f32_e32 v10, v54, v10
	s_nop 0
	v_lshlrev_b32_e32 v54, 16, v117
	v_mul_f32_e32 v54, v191, v54
	v_fmac_f32_e32 v54, v189, v116
	v_fmac_f32_e32 v54, v192, v15
	v_add_f32_e32 v15, v193, v54
	v_add_co_u32_e32 v54, vcc, 0x4000, v2
	v_add_f32_e32 v10, v55, v10
	s_nop 0
	v_addc_co_u32_e32 v55, vcc, 0, v3, vcc
	v_mov_b32_e32 v54, v198
	s_and_b64 vcc, exec, s[4:5]
	s_nop 0
	v_mul_f32_e32 v54, v13, v54
	v_fmac_f32_e32 v54, v194, v10
	v_mul_f32_e32 v10, v15, v54
	s_cbranch_vccnz .LBB0_2800
	v_bfe_u32 v15, v10, 16, 1
	v_add3_u32 v15, v10, v15, s33
	v_lshl_add_u64 v[54:55], v[114:115], 1, s[54:55]
	s_mov_b64 s[2:3], 0
	global_store_short_d16_hi v[54:55], v15, off

.LBB0_2806:
	s_or_b64 exec, exec, s[2:3]
	v_pk_add_f32 v[54:55], v[66:67], v[70:71] neg_lo:[0,1] neg_hi:[0,1]
	v_pk_add_f32 v[66:67], v[68:69], v[72:73] neg_lo:[0,1] neg_hi:[0,1]
	s_mov_b32 s2, s75
	s_mov_b32 s3, s74
	v_xor_b32_e32 v56, 0x80000000, v67
	v_mov_b32_e32 v57, v66
	v_pk_mul_f32 v[68:69], v[18:19], s[2:3]
	v_pk_add_f32 v[66:67], v[54:55], v[56:57]
	v_pk_fma_f32 v[68:69], v[16:17], s[74:75], v[68:69]
	s_mov_b64 s[2:3], -1
	v_pk_mul_f32 v[66:67], v[68:69], v[66:67]
	v_add_f32_e32 v10, v66, v10
	s_nop 0
	v_lshlrev_b32_e32 v66, 16, v117
	v_mul_f32_e32 v66, v191, v66
	v_fmac_f32_e32 v66, v189, v116
	v_fmac_f32_e32 v66, v192, v15
	v_add_f32_e32 v15, v193, v66
	v_add_co_u32_e32 v66, vcc, 0x4000, v2
	v_add_f32_e32 v10, v67, v10
	s_nop 0
	v_addc_co_u32_e32 v67, vcc, 0, v3, vcc
	v_mov_b32_e32 v66, v203
	s_and_b64 vcc, exec, s[4:5]
	s_nop 0
	v_mul_f32_e32 v66, v13, v66
	v_fmac_f32_e32 v66, v194, v10
	v_mul_f32_e32 v10, v15, v66
	s_cbranch_vccnz .LBB0_2808
	v_bfe_u32 v15, v10, 16, 1
	v_add3_u32 v15, v10, v15, s33
	v_lshl_add_u64 v[66:67], v[114:115], 1, s[54:55]
	s_mov_b64 s[2:3], 0
	global_store_short_d16_hi v[66:67], v15, off

.LBB0_2814:
	s_or_b64 exec, exec, s[2:3]
	v_pk_add_f32 v[58:59], v[58:59], v[62:63] neg_lo:[0,1] neg_hi:[0,1]
	v_pk_add_f32 v[62:63], v[60:61], v[64:65] neg_lo:[0,1] neg_hi:[0,1]
	s_mov_b32 s2, s13
	s_mov_b32 s3, s12
	v_xor_b32_e32 v60, 0x80000000, v63
	v_mov_b32_e32 v61, v62
	v_pk_mul_f32 v[64:65], v[18:19], s[2:3]
	v_pk_add_f32 v[62:63], v[58:59], v[60:61]
	v_pk_fma_f32 v[64:65], v[16:17], s[12:13], v[64:65]
	s_mov_b64 s[2:3], -1
	v_pk_mul_f32 v[62:63], v[64:65], v[62:63]
	v_add_f32_e32 v10, v62, v10
	s_nop 0
	v_lshlrev_b32_e32 v62, 16, v69
	v_mul_f32_e32 v62, v191, v62
	v_fmac_f32_e32 v62, v189, v68
	v_fmac_f32_e32 v62, v192, v15
	v_add_f32_e32 v15, v193, v62
	v_add_co_u32_e32 v62, vcc, 0x5000, v2
	v_add_f32_e32 v10, v63, v10
	s_nop 0
	v_addc_co_u32_e32 v63, vcc, 0, v3, vcc
	v_mov_b32_e32 v62, v208
	s_and_b64 vcc, exec, s[4:5]
	s_nop 0
	v_mul_f32_e32 v62, v13, v62
	v_fmac_f32_e32 v62, v194, v10
	v_mul_f32_e32 v10, v15, v62
	s_cbranch_vccnz .LBB0_2816
	v_bfe_u32 v15, v10, 16, 1
	v_add3_u32 v15, v10, v15, s33
	v_lshl_add_u64 v[62:63], v[66:67], 1, s[54:55]
	s_mov_b64 s[2:3], 0
	global_store_short_d16_hi v[62:63], v15, off

.LBB0_2862:
	s_or_b64 exec, exec, s[2:3]
	s_mov_b32 s2, s77
	s_mov_b32 s3, s43
	v_pk_add_f32 v[4:5], v[4:5], v[6:7] neg_lo:[0,1] neg_hi:[0,1]
	s_mov_b32 s76, s43
	v_pk_mul_f32 v[6:7], v[18:19], s[2:3]
	s_mov_b64 s[2:3], -1
	v_pk_fma_f32 v[6:7], v[16:17], s[76:77], v[6:7]
	v_pk_mul_f32 v[4:5], v[6:7], v[4:5]
	v_add_f32_e32 v4, v4, v10
	v_add_f32_e32 v6, v5, v4
	s_nop 0
	v_lshlrev_b32_e32 v4, 16, v85
	v_mul_f32_e32 v4, v191, v4
	v_fmac_f32_e32 v4, v189, v84
	v_fmac_f32_e32 v4, v192, v15
	v_add_f32_e32 v7, v193, v4
	v_add_co_u32_e32 v4, vcc, 0x8000, v2
	s_nop 1
	v_addc_co_u32_e32 v5, vcc, 0, v3, vcc
	v_mov_b32_e32 v4, v198
	s_and_b64 vcc, exec, s[4:5]
	s_nop 0
	v_mul_f32_e32 v4, v13, v4
	v_fmac_f32_e32 v4, v194, v6
	v_mul_f32_e32 v4, v7, v4
	s_cbranch_vccnz .LBB0_2864
	v_bfe_u32 v5, v4, 16, 1
	v_add3_u32 v5, v4, v5, s33
	v_lshl_add_u64 v[6:7], v[82:83], 1, s[54:55]
	s_mov_b64 s[2:3], 0
	global_store_short_d16_hi v[6:7], v5, off

.LBB0_2870:
	s_or_b64 exec, exec, s[2:3]
	s_mov_b32 s6, s31
	s_mov_b32 s7, s69
	v_pk_add_f32 v[26:27], v[26:27], v[28:29] neg_lo:[0,1] neg_hi:[0,1]
	s_mov_b32 s2, s69
	s_mov_b32 s3, s31
	v_pk_mul_f32 v[28:29], v[18:19], s[6:7]
	v_pk_fma_f32 v[28:29], v[16:17], s[2:3], v[28:29]
	s_mov_b64 s[2:3], -1
	v_pk_mul_f32 v[26:27], v[28:29], v[26:27]
	v_add_f32_e32 v6, v26, v6
	v_add_f32_e32 v26, v27, v6
	s_nop 0
	v_lshlrev_b32_e32 v6, 16, v15
	v_mul_f32_e32 v6, v191, v6
	v_fmac_f32_e32 v6, v189, v10
	v_fmac_f32_e32 v6, v192, v7
	v_add_f32_e32 v10, v193, v6
	v_add_co_u32_e32 v6, vcc, 0x8000, v2
	s_nop 1
	v_addc_co_u32_e32 v7, vcc, 0, v3, vcc
	v_mov_b32_e32 v6, v203
	s_and_b64 vcc, exec, s[4:5]
	s_nop 0
	v_mul_f32_e32 v6, v13, v6
	v_fmac_f32_e32 v6, v194, v26
	v_mul_f32_e32 v6, v10, v6
	s_cbranch_vccnz .LBB0_2872
	v_bfe_u32 v7, v6, 16, 1
	v_add3_u32 v7, v6, v7, s33
	v_lshl_add_u64 v[4:5], v[4:5], 1, s[54:55]
	s_mov_b64 s[2:3], 0
	global_store_short_d16_hi v[4:5], v7, off

.LBB0_2878:
	s_or_b64 exec, exec, s[2:3]
	s_mov_b32 s6, s89
	s_mov_b32 s7, s71
	v_pk_add_f32 v[8:9], v[8:9], v[24:25] neg_lo:[0,1] neg_hi:[0,1]
	s_mov_b32 s2, s71
	s_mov_b32 s3, s89
	v_pk_mul_f32 v[24:25], v[18:19], s[6:7]
	v_pk_fma_f32 v[24:25], v[16:17], s[2:3], v[24:25]
	s_mov_b64 s[2:3], -1
	v_pk_mul_f32 v[8:9], v[24:25], v[8:9]
	v_add_f32_e32 v6, v8, v6
	v_add_f32_e32 v8, v9, v6
	s_nop 0
	v_lshlrev_b32_e32 v6, 16, v15
	v_mul_f32_e32 v6, v191, v6
	v_fmac_f32_e32 v6, v189, v10
	v_fmac_f32_e32 v6, v192, v7
	v_add_f32_e32 v9, v193, v6
	v_add_co_u32_e32 v6, vcc, 0x9000, v2
	s_nop 1
	v_addc_co_u32_e32 v7, vcc, 0, v3, vcc
	v_mov_b32_e32 v6, v208
	s_and_b64 vcc, exec, s[4:5]
	s_nop 0
	v_mul_f32_e32 v6, v13, v6
	v_fmac_f32_e32 v6, v194, v8
	v_mul_f32_e32 v6, v9, v6
	s_cbranch_vccnz .LBB0_2880
	v_bfe_u32 v7, v6, 16, 1
	v_add3_u32 v7, v6, v7, s33
	v_lshl_add_u64 v[4:5], v[4:5], 1, s[54:55]
	s_mov_b64 s[2:3], 0
	global_store_short_d16_hi v[4:5], v7, off

.LBB0_2886:
	s_or_b64 exec, exec, s[2:3]
	s_mov_b32 s6, s87
	s_mov_b32 s7, s41
	s_mov_b32 s2, s41
	s_mov_b32 s3, s87
	v_pk_mul_f32 v[26:27], v[18:19], s[6:7]
	v_pk_add_f32 v[24:25], v[30:31], v[32:33] neg_lo:[0,1] neg_hi:[0,1]
	v_pk_fma_f32 v[26:27], v[16:17], s[2:3], v[26:27]
	s_mov_b64 s[2:3], -1
	v_pk_mul_f32 v[24:25], v[26:27], v[24:25]
	v_add_f32_e32 v6, v24, v6
	v_add_f32_e32 v10, v25, v6
	s_nop 0
	v_lshlrev_b32_e32 v6, 16, v9
	v_mul_f32_e32 v6, v191, v6
	v_fmac_f32_e32 v6, v189, v8
	v_fmac_f32_e32 v6, v192, v7
	v_add_f32_e32 v8, v193, v6
	v_add_co_u32_e32 v6, vcc, 0x9000, v2
	s_nop 1
	v_addc_co_u32_e32 v7, vcc, 0, v3, vcc
	v_mov_b32_e32 v6, v213
	s_and_b64 vcc, exec, s[4:5]
	s_nop 0
	v_mul_f32_e32 v6, v13, v6
	v_fmac_f32_e32 v6, v194, v10
	v_mul_f32_e32 v6, v8, v6
	s_cbranch_vccnz .LBB0_2888
	v_bfe_u32 v7, v6, 16, 1
	v_add3_u32 v7, v6, v7, s33
	v_lshl_add_u64 v[4:5], v[4:5], 1, s[54:55]
	s_mov_b64 s[2:3], 0
	global_store_short_d16_hi v[4:5], v7, off

.LBB0_2894:
	s_or_b64 exec, exec, s[2:3]
	s_mov_b32 s6, s85
	s_mov_b32 s7, s95
	s_mov_b32 s2, s95
	s_mov_b32 s3, s85
	v_pk_mul_f32 v[26:27], v[18:19], s[6:7]
	v_pk_add_f32 v[24:25], v[34:35], v[36:37] neg_lo:[0,1] neg_hi:[0,1]
	v_pk_fma_f32 v[26:27], v[16:17], s[2:3], v[26:27]
	s_mov_b64 s[2:3], -1
	v_pk_mul_f32 v[24:25], v[26:27], v[24:25]
	v_add_f32_e32 v6, v24, v6
	v_add_f32_e32 v10, v25, v6
	s_nop 0
	v_lshlrev_b32_e32 v6, 16, v9
	v_mul_f32_e32 v6, v191, v6
	v_fmac_f32_e32 v6, v189, v8
	v_fmac_f32_e32 v6, v192, v7
	v_add_f32_e32 v8, v193, v6
	v_add_co_u32_e32 v6, vcc, 0xa000, v2
	s_nop 1
	v_addc_co_u32_e32 v7, vcc, 0, v3, vcc
	v_mov_b32_e32 v6, v218
	s_and_b64 vcc, exec, s[4:5]
	s_nop 0
	v_mul_f32_e32 v6, v13, v6
	v_fmac_f32_e32 v6, v194, v10
	v_mul_f32_e32 v6, v8, v6
	s_cbranch_vccnz .LBB0_2896
	v_bfe_u32 v7, v6, 16, 1
	v_add3_u32 v7, v6, v7, s33
	v_lshl_add_u64 v[4:5], v[4:5], 1, s[54:55]
	s_mov_b64 s[2:3], 0
	global_store_short_d16_hi v[4:5], v7, off

.LBB0_2902:
	s_or_b64 exec, exec, s[2:3]
	s_mov_b32 s6, s83
	s_mov_b32 s7, s79
	s_mov_b32 s2, s79
	s_mov_b32 s3, s83
	v_pk_mul_f32 v[26:27], v[18:19], s[6:7]
	v_pk_add_f32 v[24:25], v[38:39], v[40:41] neg_lo:[0,1] neg_hi:[0,1]
	v_pk_fma_f32 v[26:27], v[16:17], s[2:3], v[26:27]
	s_mov_b64 s[2:3], -1
	v_pk_mul_f32 v[24:25], v[26:27], v[24:25]
	v_add_f32_e32 v6, v24, v6
	v_add_f32_e32 v10, v25, v6
	s_nop 0
	v_lshlrev_b32_e32 v6, 16, v9
	v_mul_f32_e32 v6, v191, v6
	v_fmac_f32_e32 v6, v189, v8
	v_fmac_f32_e32 v6, v192, v7
	v_add_f32_e32 v8, v193, v6
	v_add_co_u32_e32 v6, vcc, 0xa000, v2
	s_nop 1
	v_addc_co_u32_e32 v7, vcc, 0, v3, vcc
	v_mov_b32_e32 v6, v223
	s_and_b64 vcc, exec, s[4:5]
	s_nop 0
	v_mul_f32_e32 v6, v13, v6
	v_fmac_f32_e32 v6, v194, v10
	v_mul_f32_e32 v6, v8, v6
	s_cbranch_vccnz .LBB0_2904
	v_bfe_u32 v7, v6, 16, 1
	v_add3_u32 v7, v6, v7, s33
	v_lshl_add_u64 v[4:5], v[4:5], 1, s[54:55]
	s_mov_b64 s[2:3], 0
	global_store_short_d16_hi v[4:5], v7, off

.LBB0_2910:
	s_or_b64 exec, exec, s[2:3]
	s_mov_b32 s6, s13
	s_mov_b32 s7, s81
	s_mov_b32 s2, s81
	s_mov_b32 s3, s13
	v_pk_mul_f32 v[26:27], v[18:19], s[6:7]
	v_pk_add_f32 v[24:25], v[42:43], v[44:45] neg_lo:[0,1] neg_hi:[0,1]
	v_pk_fma_f32 v[26:27], v[16:17], s[2:3], v[26:27]
	s_mov_b64 s[2:3], -1
	v_pk_mul_f32 v[24:25], v[26:27], v[24:25]
	v_add_f32_e32 v6, v24, v6
	v_add_f32_e32 v10, v25, v6
	s_nop 0
	v_lshlrev_b32_e32 v6, 16, v9
	v_mul_f32_e32 v6, v191, v6
	v_fmac_f32_e32 v6, v189, v8
	v_fmac_f32_e32 v6, v192, v7
	v_add_f32_e32 v8, v193, v6
	v_add_co_u32_e32 v6, vcc, 0xb000, v2
	s_nop 1
	v_addc_co_u32_e32 v7, vcc, 0, v3, vcc
	v_mov_b32_e32 v6, v228
	s_and_b64 vcc, exec, s[4:5]
	s_nop 0
	v_mul_f32_e32 v6, v13, v6
	v_fmac_f32_e32 v6, v194, v10
	v_mul_f32_e32 v6, v8, v6
	s_cbranch_vccnz .LBB0_2912
	v_bfe_u32 v7, v6, 16, 1
	v_add3_u32 v7, v6, v7, s33
	v_lshl_add_u64 v[4:5], v[4:5], 1, s[54:55]
	s_mov_b64 s[2:3], 0
	global_store_short_d16_hi v[4:5], v7, off

.LBB0_2918:
	s_or_b64 exec, exec, s[2:3]
	s_mov_b32 s6, s75
	s_mov_b32 s7, s9
	s_mov_b32 s2, s9
	s_mov_b32 s3, s75
	v_pk_mul_f32 v[26:27], v[18:19], s[6:7]
	v_pk_add_f32 v[24:25], v[46:47], v[48:49] neg_lo:[0,1] neg_hi:[0,1]
	v_pk_fma_f32 v[26:27], v[16:17], s[2:3], v[26:27]
	s_mov_b64 s[2:3], -1
	v_pk_mul_f32 v[24:25], v[26:27], v[24:25]
	v_add_f32_e32 v6, v24, v6
	v_add_f32_e32 v10, v25, v6
	s_nop 0
	v_lshlrev_b32_e32 v6, 16, v9
	v_mul_f32_e32 v6, v191, v6
	v_fmac_f32_e32 v6, v189, v8
	v_fmac_f32_e32 v6, v192, v7
	v_add_f32_e32 v8, v193, v6
	v_add_co_u32_e32 v6, vcc, 0xb000, v2
	s_nop 1
	v_addc_co_u32_e32 v7, vcc, 0, v3, vcc
	v_mov_b32_e32 v6, v233
	s_and_b64 vcc, exec, s[4:5]
	s_nop 0
	v_mul_f32_e32 v6, v13, v6
	v_fmac_f32_e32 v6, v194, v10
	v_mul_f32_e32 v6, v8, v6
	s_cbranch_vccnz .LBB0_2920
	v_bfe_u32 v7, v6, 16, 1
	v_add3_u32 v7, v6, v7, s33
	v_lshl_add_u64 v[4:5], v[4:5], 1, s[54:55]
	s_mov_b64 s[2:3], 0
	global_store_short_d16_hi v[4:5], v7, off

.LBB0_2926:
	s_or_b64 exec, exec, s[2:3]
	s_mov_b32 s2, s53
	v_pk_mul_f32 v[26:27], v[18:19], s[2:3] op_sel_hi:[1,0]
	v_pk_add_f32 v[24:25], v[50:51], v[52:53] neg_lo:[0,1] neg_hi:[0,1]
	v_pk_fma_f32 v[26:27], v[16:17], s[2:3], v[26:27] op_sel_hi:[1,0,1]
	s_mov_b64 s[2:3], -1
	v_pk_mul_f32 v[24:25], v[26:27], v[24:25]
	v_add_f32_e32 v6, v24, v6
	v_add_f32_e32 v10, v25, v6
	s_nop 0
	v_lshlrev_b32_e32 v6, 16, v9
	v_mul_f32_e32 v6, v191, v6
	v_fmac_f32_e32 v6, v189, v8
	v_fmac_f32_e32 v6, v192, v7
	v_add_f32_e32 v8, v193, v6
	v_add_co_u32_e32 v6, vcc, 0xc000, v2
	s_nop 1
	v_addc_co_u32_e32 v7, vcc, 0, v3, vcc
	v_mov_b32_e32 v6, v198
	s_and_b64 vcc, exec, s[4:5]
	s_nop 0
	v_mul_f32_e32 v6, v13, v6
	v_fmac_f32_e32 v6, v194, v10
	v_mul_f32_e32 v6, v8, v6
	s_cbranch_vccnz .LBB0_2928
	v_bfe_u32 v7, v6, 16, 1
	v_add3_u32 v7, v6, v7, s33
	v_lshl_add_u64 v[4:5], v[4:5], 1, s[54:55]
	s_mov_b64 s[2:3], 0
	global_store_short_d16_hi v[4:5], v7, off

.LBB0_2934:
	s_or_b64 exec, exec, s[2:3]
	s_mov_b32 s6, s9
	s_mov_b32 s7, s75
	s_mov_b32 s2, s75
	s_mov_b32 s3, s9
	v_pk_mul_f32 v[26:27], v[18:19], s[6:7]
	v_pk_add_f32 v[24:25], v[54:55], v[56:57] neg_lo:[0,1] neg_hi:[0,1]
	v_pk_fma_f32 v[26:27], v[16:17], s[2:3], v[26:27]
	s_mov_b64 s[2:3], -1
	v_pk_mul_f32 v[24:25], v[26:27], v[24:25]
	v_add_f32_e32 v6, v24, v6
	v_add_f32_e32 v10, v25, v6
	s_nop 0
	v_lshlrev_b32_e32 v6, 16, v9
	v_mul_f32_e32 v6, v191, v6
	v_fmac_f32_e32 v6, v189, v8
	v_fmac_f32_e32 v6, v192, v7
	v_add_f32_e32 v8, v193, v6
	v_add_co_u32_e32 v6, vcc, 0xc000, v2
	s_nop 1
	v_addc_co_u32_e32 v7, vcc, 0, v3, vcc
	v_mov_b32_e32 v6, v203
	s_and_b64 vcc, exec, s[4:5]
	s_nop 0
	v_mul_f32_e32 v6, v13, v6
	v_fmac_f32_e32 v6, v194, v10
	v_mul_f32_e32 v6, v8, v6
	s_cbranch_vccnz .LBB0_2936
	v_bfe_u32 v7, v6, 16, 1
	v_add3_u32 v7, v6, v7, s33
	v_lshl_add_u64 v[4:5], v[4:5], 1, s[54:55]
	s_mov_b64 s[2:3], 0
	global_store_short_d16_hi v[4:5], v7, off

.LBB0_2942:
	s_or_b64 exec, exec, s[2:3]
	s_mov_b32 s6, s81
	s_mov_b32 s7, s13
	s_mov_b32 s2, s13
	s_mov_b32 s3, s81
	v_pk_mul_f32 v[26:27], v[18:19], s[6:7]
	v_pk_add_f32 v[24:25], v[58:59], v[60:61] neg_lo:[0,1] neg_hi:[0,1]
	v_pk_fma_f32 v[26:27], v[16:17], s[2:3], v[26:27]
	s_mov_b64 s[2:3], -1
	v_pk_mul_f32 v[24:25], v[26:27], v[24:25]
	v_add_f32_e32 v6, v24, v6
	v_add_f32_e32 v10, v25, v6
	s_nop 0
	v_lshlrev_b32_e32 v6, 16, v9
	v_mul_f32_e32 v6, v191, v6
	v_fmac_f32_e32 v6, v189, v8
	v_fmac_f32_e32 v6, v192, v7
	v_add_f32_e32 v8, v193, v6
	v_add_co_u32_e32 v6, vcc, 0xd000, v2
	s_nop 1
	v_addc_co_u32_e32 v7, vcc, 0, v3, vcc
	v_mov_b32_e32 v6, v208
	s_and_b64 vcc, exec, s[4:5]
	s_nop 0
	v_mul_f32_e32 v6, v13, v6
	v_fmac_f32_e32 v6, v194, v10
	v_mul_f32_e32 v6, v8, v6
	s_cbranch_vccnz .LBB0_2944
	v_bfe_u32 v7, v6, 16, 1
	v_add3_u32 v7, v6, v7, s33
	v_lshl_add_u64 v[4:5], v[4:5], 1, s[54:55]
	s_mov_b64 s[2:3], 0
	global_store_short_d16_hi v[4:5], v7, off

.LBB0_2950:
	s_or_b64 exec, exec, s[2:3]
	s_mov_b32 s6, s79
	s_mov_b32 s7, s83
	s_mov_b32 s2, s83
	s_mov_b32 s3, s79
	v_pk_mul_f32 v[26:27], v[18:19], s[6:7]
	v_pk_add_f32 v[24:25], v[62:63], v[64:65] neg_lo:[0,1] neg_hi:[0,1]
	v_pk_fma_f32 v[26:27], v[16:17], s[2:3], v[26:27]
	s_mov_b64 s[2:3], -1
	v_pk_mul_f32 v[24:25], v[26:27], v[24:25]
	v_add_f32_e32 v6, v24, v6
	v_add_f32_e32 v10, v25, v6
	s_nop 0
	v_lshlrev_b32_e32 v6, 16, v9
	v_mul_f32_e32 v6, v191, v6
	v_fmac_f32_e32 v6, v189, v8
	v_fmac_f32_e32 v6, v192, v7
	v_add_f32_e32 v8, v193, v6
	v_add_co_u32_e32 v6, vcc, 0xd000, v2
	s_nop 1
	v_addc_co_u32_e32 v7, vcc, 0, v3, vcc
	v_mov_b32_e32 v6, v213
	s_and_b64 vcc, exec, s[4:5]
	s_nop 0
	v_mul_f32_e32 v6, v13, v6
	v_fmac_f32_e32 v6, v194, v10
	v_mul_f32_e32 v6, v8, v6
	s_cbranch_vccnz .LBB0_2952
	v_bfe_u32 v7, v6, 16, 1
	v_add3_u32 v7, v6, v7, s33
	v_lshl_add_u64 v[4:5], v[4:5], 1, s[54:55]
	s_mov_b64 s[2:3], 0
	global_store_short_d16_hi v[4:5], v7, off

.LBB0_2958:
	s_or_b64 exec, exec, s[2:3]
	s_mov_b32 s6, s95
	s_mov_b32 s7, s85
	s_mov_b32 s2, s85
	s_mov_b32 s3, s95
	v_pk_mul_f32 v[26:27], v[18:19], s[6:7]
	v_pk_add_f32 v[24:25], v[66:67], v[68:69] neg_lo:[0,1] neg_hi:[0,1]
	v_pk_fma_f32 v[26:27], v[16:17], s[2:3], v[26:27]
	s_mov_b64 s[2:3], -1
	v_pk_mul_f32 v[24:25], v[26:27], v[24:25]
	v_add_f32_e32 v6, v24, v6
	v_add_f32_e32 v10, v25, v6
	s_nop 0
	v_lshlrev_b32_e32 v6, 16, v9
	v_mul_f32_e32 v6, v191, v6
	v_fmac_f32_e32 v6, v189, v8
	v_fmac_f32_e32 v6, v192, v7
	v_add_f32_e32 v8, v193, v6
	v_add_co_u32_e32 v6, vcc, 0xe000, v2
	s_nop 1
	v_addc_co_u32_e32 v7, vcc, 0, v3, vcc
	v_mov_b32_e32 v6, v218
	s_and_b64 vcc, exec, s[4:5]
	s_nop 0
	v_mul_f32_e32 v6, v13, v6
	v_fmac_f32_e32 v6, v194, v10
	v_mul_f32_e32 v6, v8, v6
	s_cbranch_vccnz .LBB0_2960
	v_bfe_u32 v7, v6, 16, 1
	v_add3_u32 v7, v6, v7, s33
	v_lshl_add_u64 v[4:5], v[4:5], 1, s[54:55]
	s_mov_b64 s[2:3], 0
	global_store_short_d16_hi v[4:5], v7, off

.LBB0_2966:
	s_or_b64 exec, exec, s[2:3]
	s_mov_b32 s6, s41
	s_mov_b32 s7, s87
	s_mov_b32 s2, s87
	s_mov_b32 s3, s41
	v_pk_mul_f32 v[26:27], v[18:19], s[6:7]
	v_pk_add_f32 v[24:25], v[70:71], v[72:73] neg_lo:[0,1] neg_hi:[0,1]
	v_pk_fma_f32 v[26:27], v[16:17], s[2:3], v[26:27]
	s_mov_b64 s[2:3], -1
	v_pk_mul_f32 v[24:25], v[26:27], v[24:25]
	v_add_f32_e32 v6, v24, v6
	v_add_f32_e32 v10, v25, v6
	s_nop 0
	v_lshlrev_b32_e32 v6, 16, v9
	v_mul_f32_e32 v6, v191, v6
	v_fmac_f32_e32 v6, v189, v8
	v_fmac_f32_e32 v6, v192, v7
	v_add_f32_e32 v8, v193, v6
	v_add_co_u32_e32 v6, vcc, 0xe000, v2
	s_nop 1
	v_addc_co_u32_e32 v7, vcc, 0, v3, vcc
	v_mov_b32_e32 v6, v223
	s_and_b64 vcc, exec, s[4:5]
	s_nop 0
	v_mul_f32_e32 v6, v13, v6
	v_fmac_f32_e32 v6, v194, v10
	v_mul_f32_e32 v6, v8, v6
	s_cbranch_vccnz .LBB0_2968
	v_bfe_u32 v7, v6, 16, 1
	v_add3_u32 v7, v6, v7, s33
	v_lshl_add_u64 v[4:5], v[4:5], 1, s[54:55]
	s_mov_b64 s[2:3], 0
	global_store_short_d16_hi v[4:5], v7, off

.LBB0_2974:
	s_or_b64 exec, exec, s[2:3]
	s_mov_b32 s6, s71
	s_mov_b32 s7, s89
	s_mov_b32 s2, s89
	s_mov_b32 s3, s71
	v_pk_mul_f32 v[26:27], v[18:19], s[6:7]
	v_pk_add_f32 v[24:25], v[74:75], v[76:77] neg_lo:[0,1] neg_hi:[0,1]
	v_pk_fma_f32 v[26:27], v[16:17], s[2:3], v[26:27]
	s_mov_b64 s[2:3], -1
	v_pk_mul_f32 v[24:25], v[26:27], v[24:25]
	v_add_f32_e32 v6, v24, v6
	v_add_f32_e32 v10, v25, v6
	s_nop 0
	v_lshlrev_b32_e32 v6, 16, v9
	v_mul_f32_e32 v6, v191, v6
	v_fmac_f32_e32 v6, v189, v8
	v_fmac_f32_e32 v6, v192, v7
	v_add_f32_e32 v8, v193, v6
	v_add_co_u32_e32 v6, vcc, 0xf000, v2
	s_nop 1
	v_addc_co_u32_e32 v7, vcc, 0, v3, vcc
	v_mov_b32_e32 v6, v228
	s_and_b64 vcc, exec, s[4:5]
	s_nop 0
	v_mul_f32_e32 v6, v13, v6
	v_fmac_f32_e32 v6, v194, v10
	v_mul_f32_e32 v6, v8, v6
	s_cbranch_vccnz .LBB0_2976
	v_bfe_u32 v7, v6, 16, 1
	v_add3_u32 v7, v6, v7, s33
	v_lshl_add_u64 v[4:5], v[4:5], 1, s[54:55]
	s_mov_b64 s[2:3], 0
	global_store_short_d16_hi v[4:5], v7, off

.LBB0_2982:
	s_or_b64 exec, exec, s[0:1]
	s_mov_b32 s2, s69
	s_mov_b32 s3, s31
	s_mov_b32 s0, s31
	s_mov_b32 s1, s69
	v_pk_mul_f32 v[18:19], v[18:19], s[2:3]
	v_pk_add_f32 v[14:15], v[78:79], v[80:81] neg_lo:[0,1] neg_hi:[0,1]
	v_pk_fma_f32 v[16:17], v[16:17], s[0:1], v[18:19]
	s_mov_b64 s[0:1], -1
	v_pk_mul_f32 v[14:15], v[16:17], v[14:15]
	v_add_f32_e32 v6, v14, v6
	v_add_f32_e32 v10, v15, v6
	s_nop 0
	v_lshlrev_b32_e32 v6, 16, v9
	v_mul_f32_e32 v6, v191, v6
	v_fmac_f32_e32 v6, v189, v8
	v_fmac_f32_e32 v6, v192, v7
	v_add_f32_e32 v8, v193, v6
	v_add_co_u32_e32 v6, vcc, 0xf000, v2
	s_nop 1
	v_addc_co_u32_e32 v7, vcc, 0, v3, vcc
	v_mov_b32_e32 v6, v233
	s_and_b64 vcc, exec, s[4:5]
	s_nop 0
	v_mul_f32_e32 v6, v13, v6
	v_fmac_f32_e32 v6, v194, v10
	v_mul_f32_e32 v6, v8, v6
	s_cbranch_vccnz .LBB0_2984
	v_bfe_u32 v7, v6, 16, 1
	v_add3_u32 v7, v6, v7, s33
	v_lshl_add_u64 v[4:5], v[4:5], 1, s[54:55]
	global_store_short_d16_hi v[4:5], v7, off
	s_cbranch_execnz .LBB0_2727
	s_branch .LBB0_2985
